# FFT unit: dead VGPR-only address arithmetic left behind by the load batching removed (backward liveness over the forward-branch code), hazard pads re-checked
# speedup vs baseline: 1.0236x; 1.0079x over previous
.LBB0_608:
	s_cmp_lt_i32 s54, 5
	s_cselect_b64 s[2:3], -1, 0
	v_writelane_b32 v250, s2, 60
	s_and_b64 s[0:1], s[2:3], s[0:1]
	s_andn2_b64 vcc, exec, s[0:1]
	v_writelane_b32 v250, s3, 61
	v_writelane_b32 v250, s76, 62
	s_nop 1
	v_writelane_b32 v251, s78, 0
	v_writelane_b32 v251, s79, 1
	v_writelane_b32 v251, s80, 2
	v_writelane_b32 v251, s81, 3
	v_writelane_b32 v251, s82, 4
	v_writelane_b32 v251, s83, 5
	v_writelane_b32 v251, s84, 6
	v_writelane_b32 v251, s85, 7
	v_writelane_b32 v251, s86, 8
	v_writelane_b32 v251, s87, 9
	v_writelane_b32 v251, s88, 10
	v_writelane_b32 v251, s89, 11
	v_writelane_b32 v251, s90, 12
	v_writelane_b32 v250, s77, 63
	v_writelane_b32 v251, s91, 13
	s_cbranch_vccnz .LBB0_1086
	v_readlane_b32 s0, v250, 0
	v_mov_b32_e32 v182, v0
	s_mov_b32 s56, s0
	v_readlane_b32 s0, v250, 39
	v_readlane_b32 s1, v250, 1
	s_mov_b64 s[58:59], s[52:53]
	v_mov_b32_e32 v1, 1.0
	v_writelane_b32 v251, s1, 14
	s_mov_b64 s[0:1], s[90:91]
	v_mov_b32_e32 v164, 0x3f7b14be
	v_writelane_b32 v251, s58, 16
	v_mov_b32_e32 v165, 0x3f6c835e
	v_mov_b32_e32 v166, 0x3f54db31
	v_mov_b32_e32 v167, 0x3f3504f3
	v_mov_b32_e32 v168, 0x3f0e39da
	v_mov_b32_e32 v169, 0x3ec3ef15
	v_mov_b32_e32 v170, 0x3e47c5c2
	s_waitcnt vmcnt(9)
	v_mov_b32_e32 v11, 0
	v_mov_b32_e32 v171, 0
	s_cmpk_gt_i32 s56, 0x3ff
	v_writelane_b32 v251, s59, 17
	s_cbranch_scc1 .LBB0_942
	v_lshrrev_b32_e32 v2, 5, v182
	v_bitop3_b32 v173, v2, v182, 15 bitop3:0x6c
	v_ashrrev_i32_e32 v2, 1, v182
	v_and_b32_e32 v2, -16, v2
	v_lshl_add_u32 v176, v182, 4, v2
	v_add_u32_e32 v2, 0x200, v182
	v_cvt_f32_i32_e32 v3, v182
	v_ashrrev_i32_e32 v4, 1, v2
	v_and_b32_e32 v172, 15, v182
	v_ashrrev_i32_e32 v10, 4, v182
	s_movk_i32 s0, 0x210
	v_and_b32_e32 v4, -16, v4
	v_mul_lo_u32 v174, v10, s0
	v_lshl_add_u32 v177, v2, 4, v4
	v_cvt_f32_ubyte0_e32 v2, v172
	s_mov_b32 s0, 0x3b000000
	v_pk_mul_f32 v[4:5], v[2:3], -2.0 op_sel_hi:[1,0]
	s_mov_b32 s1, 0x38800000
	v_pk_mul_f32 v[4:5], v[4:5], s[0:1]
	s_mov_b32 s2, 0x7f800000
	v_and_b32_e32 v7, 0x7fffffff, v5
	v_and_b32_e32 v6, 0x7fffffff, v4
	v_pk_mul_f32 v[8:9], v[6:7], 0.5 op_sel_hi:[1,0]
	v_cmp_gt_f32_e64 s[0:1], |v5|, 1.0
	v_floor_f32_e32 v2, v9
	v_sub_f32_e32 v2, v9, v2
	v_min_f32_e32 v2, 0x3f7fffff, v2
	v_add_f32_e32 v2, v2, v2
	v_cmp_neq_f32_e32 vcc, s2, v9
	v_mov_b32_e32 v13, 0xbf1f24be
	v_xor_b32_e32 v7, v7, v5
	v_cndmask_b32_e32 v2, 0, v2, vcc
	v_cndmask_b32_e64 v2, |v5|, v2, s[0:1]
	v_add_f32_e32 v9, v2, v2
	v_rndne_f32_e32 v9, v9
	v_fmac_f32_e32 v2, -0.5, v9
	v_mul_f32_e32 v12, v2, v2
	s_waitcnt vmcnt(8)
	v_fmamk_f32 v14, v12, 0x3e75aa41, v13
	v_fmaak_f32 v14, v12, v14, 0x40234736
	v_fmaak_f32 v14, v12, v14, 0xc0a55e0e
	v_mul_f32_e32 v17, v2, v12
	v_mul_f32_e32 v14, v17, v14
	v_fmac_f32_e32 v14, 0x40490fdb, v2
	v_mov_b32_e32 v2, 0x3e642e9d
	v_cvt_i32_f32_e32 v9, v9
	v_fmamk_f32 v17, v12, 0x3d4be544, v2
	v_fmaak_f32 v17, v12, v17, 0xbfaad1da
	v_fmaak_f32 v17, v12, v17, 0x4081e0d3
	v_fmaak_f32 v17, v12, v17, 0xc09de9e6
	v_fma_f32 v12, v12, v17, 1.0
	v_lshlrev_b32_e32 v17, 30, v9
	v_and_b32_e32 v9, 1, v9
	v_cmp_eq_u32_e32 vcc, 0, v9
	s_movk_i32 s3, 0x1f8
	s_brev_b32 s45, 1
	v_cndmask_b32_e32 v9, v12, v14, vcc
	v_xor_b32_e32 v7, v7, v9
	v_xor_b32_e32 v9, 0x80000000, v14
	v_cndmask_b32_e32 v9, v9, v12, vcc
	v_cmp_class_f32_e64 vcc, v5, s3
	v_floor_f32_e32 v5, v8
	s_waitcnt vmcnt(7)
	v_and_b32_e32 v21, 0x80000000, v17
	v_sub_f32_e32 v5, v8, v5
	v_xor_b32_e32 v7, v7, v21
	v_bitop3_b32 v9, v9, v17, s45 bitop3:0x78
	v_mov_b32_e32 v12, 0x7fc00000
	v_min_f32_e32 v5, 0x3f7fffff, v5
	v_cndmask_b32_e32 v178, v12, v9, vcc
	v_cndmask_b32_e32 v179, v12, v7, vcc
	v_add_f32_e32 v5, v5, v5
	v_cmp_neq_f32_e32 vcc, s2, v8
	v_cmp_gt_f32_e64 s[0:1], |v4|, 1.0
	v_xor_b32_e32 v6, v6, v4
	v_cndmask_b32_e32 v5, 0, v5, vcc
	v_cndmask_b32_e64 v5, |v4|, v5, s[0:1]
	v_add_f32_e32 v7, v5, v5
	v_rndne_f32_e32 v7, v7
	v_fmac_f32_e32 v5, -0.5, v7
	v_mul_f32_e32 v8, v5, v5
	v_fmamk_f32 v9, v8, 0x3e75aa41, v13
	v_fmaak_f32 v9, v8, v9, 0x40234736
	v_fmaak_f32 v9, v8, v9, 0xc0a55e0e
	v_mul_f32_e32 v14, v5, v8
	v_mul_f32_e32 v9, v14, v9
	v_cvt_i32_f32_e32 v7, v7
	v_fmac_f32_e32 v9, 0x40490fdb, v5
	v_fmamk_f32 v5, v8, 0x3d4be544, v2
	v_fmaak_f32 v5, v8, v5, 0xbfaad1da
	v_fmaak_f32 v5, v8, v5, 0x4081e0d3
	v_fmaak_f32 v5, v8, v5, 0xc09de9e6
	v_fma_f32 v5, v8, v5, 1.0
	v_lshlrev_b32_e32 v8, 30, v7
	v_and_b32_e32 v7, 1, v7
	v_cmp_eq_u32_e32 vcc, 0, v7
	v_and_b32_e32 v14, 0x80000000, v8
	v_mul_f32_e32 v3, 0xb8800000, v3
	v_cndmask_b32_e32 v7, v5, v9, vcc
	v_xor_b32_e32 v6, v6, v7
	v_xor_b32_e32 v7, 0x80000000, v9
	v_cndmask_b32_e32 v5, v7, v5, vcc
	v_bitop3_b32 v5, v5, v8, s45 bitop3:0x78
	v_cmp_class_f32_e64 vcc, v4, s3
	v_xor_b32_e32 v6, v6, v14
	v_cmp_gt_f32_e64 s[0:1], |v3|, 1.0
	v_cndmask_b32_e32 v180, v12, v5, vcc
	v_mul_f32_e64 v5, |v3|, 0.5
	v_cndmask_b32_e32 v181, v12, v6, vcc
	v_fract_f32_e32 v6, v5
	v_add_f32_e32 v6, v6, v6
	v_cmp_neq_f32_e32 vcc, s2, v5
	s_ashr_i32 s57, s56, 31
	v_mov_b32_e32 v15, 0x40234736
	v_cndmask_b32_e32 v5, 0, v6, vcc
	v_cndmask_b32_e64 v5, |v3|, v5, s[0:1]
	s_lshl_b64 s[0:1], s[56:57], 18
	s_add_u32 s0, s58, s0
	s_addc_u32 s1, s59, s1
	s_add_u32 s46, s0, 0x2a940000
	s_addc_u32 s47, s1, 0
	s_add_u32 s64, s0, 0x2a960000
	v_add_f32_e32 v6, v5, v5
	s_addc_u32 s65, s1, 0
	v_rndne_f32_e32 v6, v6
	s_add_u32 s2, s58, 0x3f040000
	v_fmac_f32_e32 v5, -0.5, v6
	v_writelane_b32 v251, s2, 18
	s_addc_u32 s2, s59, 0
	v_mul_f32_e32 v7, v5, v5
	s_add_u32 s0, s0, 0x2a970000
	v_cvt_i32_f32_e32 v6, v6
	v_fmac_f32_e32 v13, 0x3e75aa41, v7
	v_writelane_b32 v251, s2, 20
	s_addc_u32 s1, s1, 0
	v_mov_b32_e32 v16, 0xc0a55e0e
	v_mov_b32_e32 v18, 0xbfaad1da
	v_fmac_f32_e32 v15, v7, v13
	v_fmac_f32_e32 v2, 0x3d4be544, v7
	v_writelane_b32 v251, s0, 22
	v_mov_b32_e32 v19, 0x4081e0d3
	v_fmac_f32_e32 v16, v7, v15
	v_mul_f32_e32 v8, v5, v7
	v_fmac_f32_e32 v18, v7, v2
	v_writelane_b32 v251, s1, 23
	s_add_u32 s0, s58, 0x22940000
	v_mov_b32_e32 v20, 0xc09de9e6
	v_mul_f32_e32 v8, v8, v16
	v_fmac_f32_e32 v19, v7, v18
	v_writelane_b32 v251, s0, 24
	s_addc_u32 s0, s59, 0
	v_fmac_f32_e32 v8, 0x40490fdb, v5
	v_fmac_f32_e32 v20, v7, v19
	v_lshlrev_b32_e32 v5, 30, v6
	v_and_b32_e32 v6, 1, v6
	v_writelane_b32 v251, s0, 26
	s_add_i32 s0, 0, 0x21000
	v_and_b32_e32 v4, 0x7fffffff, v3
	v_fma_f32 v2, v7, v20, 1.0
	v_cmp_eq_u32_e32 vcc, 0, v6
	v_writelane_b32 v251, s0, 28
	v_add_u32_e32 v186, s0, v10
	s_add_u32 s0, s58, 0x3af40000
	v_cndmask_b32_e32 v6, v2, v8, vcc
	v_xor_b32_e32 v4, v4, v3
	v_writelane_b32 v251, s0, 30
	s_addc_u32 s0, s59, 0
	s_mul_i32 s1, s56, 0x8200
	v_xor_b32_e32 v4, v4, v6
	v_xor_b32_e32 v6, 0x80000000, v8
	v_writelane_b32 v251, s0, 32
	s_mul_hi_i32 s0, s56, 0x8200
	s_add_u32 s1, s58, s1
	v_cndmask_b32_e32 v2, v6, v2, vcc
	s_addc_u32 s0, s59, s0
	v_bitop3_b32 v2, v2, v5, s45 bitop3:0x78
	v_cmp_class_f32_e64 vcc, v3, s3
	s_add_u32 s20, s1, 0x3f040800
	s_addc_u32 s21, s0, 0
	v_cndmask_b32_e32 v183, v12, v2, vcc
	v_and_b32_e32 v2, 63, v182
	s_add_i32 s0, 0, 0x21010
	v_writelane_b32 v251, s0, 34
	v_cmp_eq_u32_e64 s[0:1], 0, v2
	v_and_b32_e32 v7, 0x80000000, v5
	s_mov_b64 s[94:95], 0x3f800000
	v_writelane_b32 v251, s0, 36
	v_xor_b32_e32 v4, v4, v7
	v_mbcnt_lo_u32_b32 v3, -1, 0
	v_writelane_b32 v251, s1, 37
	s_mov_b32 s0, s56
	v_writelane_b32 v251, s0, 38
	v_bfe_u32 v175, v182, 1, 4
	v_cndmask_b32_e32 v184, v12, v4, vcc
	v_ashrrev_i32_e32 v185, 6, v182
	v_mov_b32_e32 v187, 0x3000
	v_mov_b32_e32 v188, 0x6000
	s_movk_i32 s22, 0x3fff
	s_movk_i32 s43, 0x4000
	s_movk_i32 s23, 0xfe00
	s_movk_i32 s48, 0xfc00
	s_movk_i32 s49, 0xfa00
	s_movk_i32 s50, 0xf800
	s_movk_i32 s51, 0xf600
	s_movk_i32 s57, 0xf400
	s_movk_i32 s58, 0xf200
	s_movk_i32 s59, 0xf000
	s_movk_i32 s78, 0x3000
	s_movk_i32 s60, 0xee00
	s_movk_i32 s61, 0xec00
	s_movk_i32 s62, 0xea00
	s_movk_i32 s63, 0xe800
	s_movk_i32 s66, 0xe600
	s_movk_i32 s67, 0xe400
	s_movk_i32 s68, 0xe200
	s_movk_i32 s69, 0xe000
	s_movk_i32 s74, 0xde00
	s_movk_i32 s75, 0xdc00
	s_movk_i32 s79, 0xda00
	s_movk_i32 s84, 0xce00
	s_mov_b32 s90, s45
	s_mov_b32 s91, s95
	v_mbcnt_hi_u32_b32 v189, -1, v3
	v_bfrev_b32_e32 v12, 1
	s_mov_b32 s97, -1.0
	v_writelane_b32 v251, s1, 39
	s_mov_b32 s24, s56
	s_movk_i32 s56, 0xd800
	s_movk_i32 s72, 0x4000
	s_movk_i32 s73, 0x7000
	s_branch .LBB0_612

.LBB0_634:
	s_or_b64 exec, exec, s[0:1]
	v_readlane_b32 s0, v251, 28
	v_mov_b32_e32 v90, v173
	s_nop 0
	v_mov_b32_e32 v2, s0
	v_readlane_b32 s0, v251, 34
	s_waitcnt lgkmcnt(0)
	s_nop 0
	v_mov_b32_e32 v3, s0
	s_barrier
	ds_read_b128 v[6:9], v2
	ds_read_b128 v[2:5], v3
	v_mov_b32_e32 v60, v164
	v_mov_b32_e32 v34, v165
	v_mov_b32_e32 v62, v166
	v_mov_b32_e32 v32, v167
	v_mov_b32_e32 v64, v168
	v_mov_b32_e32 v38, v169
	v_mov_b32_e32 v66, v170
	v_pk_add_f32 v[68:69], v[14:15], v[42:43]
	v_pk_add_f32 v[14:15], v[14:15], v[42:43] neg_lo:[0,1] neg_hi:[0,1]
	s_nop 0
	v_mov_b32_e32 v13, v15
	v_mov_b32_e32 v10, v14
	v_mov_b32_e32 v42, v15
	v_mov_b32_e32 v43, v11
	v_pk_mul_f32 v[14:15], v[12:13], v[66:67] op_sel_hi:[1,0] neg_lo:[0,1] neg_hi:[0,1]
	v_pk_add_f32 v[70:71], v[18:19], v[52:53]
	v_pk_fma_f32 v[42:43], v[42:43], v[60:61], v[14:15] op_sel_hi:[1,0,1]
	v_pk_add_f32 v[14:15], v[16:17], v[48:49]
	v_pk_add_f32 v[48:49], v[16:17], v[48:49] neg_lo:[0,1] neg_hi:[0,1]
	v_mov_b32_e32 v17, v11
	v_mov_b32_e32 v13, v48
	v_mov_b32_e32 v16, v48
	v_pk_mul_f32 v[54:55], v[12:13], v[38:39] op_sel_hi:[1,0] neg_lo:[0,1] neg_hi:[0,1]
	v_mov_b32_e32 v13, v49
	v_pk_add_f32 v[18:19], v[18:19], v[52:53] neg_lo:[0,1] neg_hi:[0,1]
	v_pk_fma_f32 v[16:17], v[16:17], v[34:35], v[54:55] op_sel_hi:[1,0,1]
	v_mov_b32_e32 v54, v49
	v_mov_b32_e32 v55, v11
	v_pk_mul_f32 v[48:49], v[12:13], v[64:65] op_sel_hi:[1,0] neg_lo:[0,1] neg_hi:[0,1]
	v_mov_b32_e32 v13, v18
	v_pk_fma_f32 v[48:49], v[54:55], v[62:63], v[48:49] op_sel_hi:[1,0,1]
	v_mov_b32_e32 v52, v18
	v_mov_b32_e32 v53, v11
	v_pk_mul_f32 v[54:55], v[12:13], v[32:33] op_sel_hi:[1,0] neg_lo:[0,1] neg_hi:[0,1]
	v_mov_b32_e32 v13, v19
	v_pk_fma_f32 v[52:53], v[52:53], v[32:33], v[54:55] op_sel_hi:[1,0,1]
	v_mov_b32_e32 v54, v19
	v_mov_b32_e32 v55, v11
	v_pk_add_f32 v[18:19], v[20:21], v[50:51]
	v_pk_add_f32 v[20:21], v[20:21], v[50:51] neg_lo:[0,1] neg_hi:[0,1]
	v_pk_mul_f32 v[54:55], v[54:55], v[64:65] op_sel_hi:[1,0]
	v_mov_b32_e32 v50, v20
	v_mov_b32_e32 v51, v11
	v_pk_fma_f32 v[54:55], v[12:13], v[62:63], v[54:55] op_sel_hi:[1,0,1] neg_lo:[0,1,0] neg_hi:[0,1,0]
	v_pk_mul_f32 v[50:51], v[50:51], v[38:39] op_sel_hi:[1,0]
	v_mov_b32_e32 v13, v20
	v_pk_fma_f32 v[58:59], v[12:13], v[34:35], v[50:51] op_sel_hi:[1,0,1] neg_lo:[0,1,0] neg_hi:[0,1,0]
	v_mov_b32_e32 v50, v21
	v_mov_b32_e32 v51, v11
	v_pk_mul_f32 v[50:51], v[50:51], v[66:67] op_sel_hi:[1,0]
	v_mov_b32_e32 v13, v21
	v_pk_add_f32 v[20:21], v[26:27], v[46:47]
	v_pk_add_f32 v[26:27], v[26:27], v[46:47] neg_lo:[0,1] neg_hi:[0,1]
	v_pk_fma_f32 v[56:57], v[12:13], v[60:61], v[50:51] op_sel_hi:[1,0,1] neg_lo:[0,1,0] neg_hi:[0,1,0]
	v_xor_b32_e32 v73, 0x80000000, v26
	v_mov_b32_e32 v46, v27
	v_mov_b32_e32 v47, v11
	v_mov_b32_e32 v13, v27
	v_pk_add_f32 v[26:27], v[30:31], v[44:45]
	v_pk_add_f32 v[30:31], v[30:31], v[44:45] neg_lo:[0,1] neg_hi:[0,1]
	v_pk_mul_f32 v[46:47], v[46:47], v[66:67] op_sel_hi:[1,0] neg_lo:[0,1] neg_hi:[0,1]
	v_mov_b32_e32 v44, v30
	v_mov_b32_e32 v45, v11
	v_pk_fma_f32 v[74:75], v[12:13], v[60:61], v[46:47] op_sel_hi:[1,0,1] neg_lo:[0,1,0] neg_hi:[0,1,0]
	v_pk_mul_f32 v[44:45], v[44:45], v[38:39] op_sel_hi:[1,0] neg_lo:[0,1] neg_hi:[0,1]
	v_mov_b32_e32 v13, v30
	v_pk_fma_f32 v[76:77], v[12:13], v[34:35], v[44:45] op_sel_hi:[1,0,1] neg_lo:[0,1,0] neg_hi:[0,1,0]
	v_mov_b32_e32 v44, v31
	v_mov_b32_e32 v45, v11
	v_pk_mul_f32 v[44:45], v[44:45], v[64:65] op_sel_hi:[1,0] neg_lo:[0,1] neg_hi:[0,1]
	v_mov_b32_e32 v13, v31
	v_pk_add_f32 v[30:31], v[28:29], v[40:41]
	v_pk_add_f32 v[28:29], v[28:29], v[40:41] neg_lo:[0,1] neg_hi:[0,1]
	v_pk_fma_f32 v[78:79], v[12:13], v[62:63], v[44:45] op_sel_hi:[1,0,1] neg_lo:[0,1,0] neg_hi:[0,1,0]
	v_mov_b32_e32 v13, v28
	v_mov_b32_e32 v40, v28
	v_mov_b32_e32 v41, v11
	v_pk_mul_f32 v[44:45], v[12:13], v[32:33] op_sel_hi:[1,0] neg_lo:[0,1] neg_hi:[0,1]
	v_mov_b32_e32 v13, v29
	v_pk_fma_f32 v[80:81], v[40:41], v[32:33], v[44:45] op_sel_hi:[1,0,1] neg_lo:[0,1,0] neg_hi:[0,1,0]
	v_mov_b32_e32 v40, v29
	v_pk_mul_f32 v[28:29], v[12:13], v[64:65] op_sel_hi:[1,0] neg_lo:[0,1] neg_hi:[0,1]
	v_mov_b32_e32 v45, v11
	v_pk_fma_f32 v[62:63], v[40:41], v[62:63], v[28:29] op_sel_hi:[1,0,1] neg_lo:[0,1,0] neg_hi:[0,1,0]
	v_pk_add_f32 v[28:29], v[24:25], v[36:37]
	v_pk_add_f32 v[24:25], v[24:25], v[36:37] neg_lo:[0,1] neg_hi:[0,1]
	v_mov_b32_e32 v37, v11
	v_mov_b32_e32 v13, v24
	v_mov_b32_e32 v36, v24
	v_pk_mul_f32 v[40:41], v[12:13], v[38:39] op_sel_hi:[1,0] neg_lo:[0,1] neg_hi:[0,1]
	v_mov_b32_e32 v13, v25
	v_pk_fma_f32 v[64:65], v[36:37], v[34:35], v[40:41] op_sel_hi:[1,0,1] neg_lo:[0,1,0] neg_hi:[0,1,0]
	v_mov_b32_e32 v36, v25
	v_pk_mul_f32 v[24:25], v[12:13], v[66:67] op_sel_hi:[1,0] neg_lo:[0,1] neg_hi:[0,1]
	v_mov_b32_e32 v41, v11
	v_pk_fma_f32 v[66:67], v[36:37], v[60:61], v[24:25] op_sel_hi:[1,0,1] neg_lo:[0,1,0] neg_hi:[0,1,0]
	v_pk_add_f32 v[24:25], v[68:69], v[20:21] neg_lo:[0,1] neg_hi:[0,1]
	v_pk_add_f32 v[20:21], v[68:69], v[20:21]
	v_mov_b32_e32 v13, v25
	v_mov_b32_e32 v36, v24
	v_mov_b32_e32 v40, v25
	v_pk_mul_f32 v[24:25], v[12:13], v[38:39] op_sel_hi:[1,0] neg_lo:[0,1] neg_hi:[0,1]
	v_mov_b32_e32 v69, v11
	v_pk_fma_f32 v[24:25], v[40:41], v[34:35], v[24:25] op_sel_hi:[1,0,1]
	v_pk_add_f32 v[40:41], v[14:15], v[26:27] neg_lo:[0,1] neg_hi:[0,1]
	v_pk_add_f32 v[14:15], v[14:15], v[26:27]
	v_mov_b32_e32 v13, v40
	v_mov_b32_e32 v44, v40
	v_pk_mul_f32 v[46:47], v[12:13], v[32:33] op_sel_hi:[1,0] neg_lo:[0,1] neg_hi:[0,1]
	v_mov_b32_e32 v13, v41
	v_pk_fma_f32 v[44:45], v[44:45], v[32:33], v[46:47] op_sel_hi:[1,0,1]
	v_mov_b32_e32 v46, v41
	v_mov_b32_e32 v47, v11
	v_pk_mul_f32 v[46:47], v[46:47], v[38:39] op_sel_hi:[1,0]
	v_pk_add_f32 v[40:41], v[70:71], v[30:31] neg_lo:[0,1] neg_hi:[0,1]
	v_pk_fma_f32 v[50:51], v[12:13], v[34:35], v[46:47] op_sel_hi:[1,0,1] neg_lo:[0,1,0] neg_hi:[0,1,0]
	v_mov_b32_e32 v46, v41
	v_mov_b32_e32 v47, v11
	v_xor_b32_e32 v83, 0x80000000, v40
	v_pk_mul_f32 v[46:47], v[46:47], v[38:39] op_sel_hi:[1,0] neg_lo:[0,1] neg_hi:[0,1]
	v_mov_b32_e32 v13, v41
	v_pk_add_f32 v[40:41], v[18:19], v[28:29] neg_lo:[0,1] neg_hi:[0,1]
	v_pk_fma_f32 v[84:85], v[12:13], v[34:35], v[46:47] op_sel_hi:[1,0,1] neg_lo:[0,1,0] neg_hi:[0,1,0]
	v_mov_b32_e32 v13, v40
	v_pk_add_f32 v[26:27], v[70:71], v[30:31]
	v_mov_b32_e32 v46, v40
	v_mov_b32_e32 v47, v11
	v_pk_mul_f32 v[60:61], v[12:13], v[32:33] op_sel_hi:[1,0] neg_lo:[0,1] neg_hi:[0,1]
	v_mov_b32_e32 v13, v41
	v_pk_add_f32 v[18:19], v[18:19], v[28:29]
	v_pk_add_f32 v[28:29], v[20:21], v[26:27] neg_lo:[0,1] neg_hi:[0,1]
	v_pk_fma_f32 v[86:87], v[46:47], v[32:33], v[60:61] op_sel_hi:[1,0,1] neg_lo:[0,1,0] neg_hi:[0,1,0]
	v_mov_b32_e32 v46, v41
	v_pk_mul_f32 v[40:41], v[12:13], v[38:39] op_sel_hi:[1,0] neg_lo:[0,1] neg_hi:[0,1]
	v_mov_b32_e32 v13, v29
	v_pk_fma_f32 v[88:89], v[46:47], v[34:35], v[40:41] op_sel_hi:[1,0,1] neg_lo:[0,1,0] neg_hi:[0,1,0]
	v_mov_b32_e32 v40, v28
	v_pk_add_f32 v[20:21], v[20:21], v[26:27]
	v_mov_b32_e32 v26, v29
	v_mov_b32_e32 v27, v11
	v_pk_mul_f32 v[28:29], v[12:13], v[32:33] op_sel_hi:[1,0] neg_lo:[0,1] neg_hi:[0,1]
	v_mov_b32_e32 v41, v11
	v_pk_fma_f32 v[26:27], v[26:27], v[32:33], v[28:29] op_sel_hi:[1,0,1]
	v_pk_add_f32 v[28:29], v[14:15], v[18:19] neg_lo:[0,1] neg_hi:[0,1]
	v_pk_add_f32 v[14:15], v[14:15], v[18:19]
	v_mov_b32_e32 v13, v29
	v_xor_b32_e32 v61, 0x80000000, v28
	v_mov_b32_e32 v18, v29
	v_mov_b32_e32 v19, v11
	v_pk_mul_f32 v[28:29], v[12:13], v[32:33] op_sel_hi:[1,0] neg_lo:[0,1] neg_hi:[0,1]
	v_pk_add_f32 v[30:31], v[20:21], v[14:15]
	v_pk_fma_f32 v[18:19], v[18:19], v[32:33], v[28:29] op_sel_hi:[1,0,1] neg_lo:[0,1,0] neg_hi:[0,1,0]
	v_pk_add_f32 v[28:29], v[20:21], v[14:15] neg_lo:[0,1] neg_hi:[0,1]
	v_mov_b32_e32 v60, v11
	v_pk_add_f32 v[14:15], v[28:29], 0 neg_lo:[1,1] neg_hi:[1,1]
	v_mov_b32_e32 v68, v28
	v_mov_b32_e32 v14, v11
	v_pk_add_f32 v[46:47], v[68:69], v[14:15]
	v_pk_add_f32 v[20:21], v[68:69], v[14:15] neg_lo:[0,1] neg_hi:[0,1]
	v_pk_add_f32 v[14:15], v[40:41], v[60:61]
	v_pk_add_f32 v[28:29], v[40:41], v[60:61] neg_lo:[0,1] neg_hi:[0,1]
	v_pk_add_f32 v[40:41], v[26:27], v[18:19]
	v_pk_add_f32 v[18:19], v[26:27], v[18:19] neg_lo:[0,1] neg_hi:[0,1]
	v_mov_b32_e32 v82, v11
	v_pk_add_f32 v[60:61], v[14:15], v[40:41]
	v_pk_add_f32 v[26:27], v[14:15], v[40:41] neg_lo:[0,1] neg_hi:[0,1]
	v_pk_add_f32 v[40:41], v[28:29], v[18:19] op_sel:[0,1] op_sel_hi:[1,0] neg_hi:[0,1]
	v_pk_add_f32 v[14:15], v[28:29], v[18:19] op_sel:[0,1] op_sel_hi:[1,0] neg_lo:[0,1]
	v_pk_add_f32 v[18:19], v[36:37], v[82:83]
	v_pk_add_f32 v[28:29], v[36:37], v[82:83] neg_lo:[0,1] neg_hi:[0,1]
	v_pk_add_f32 v[36:37], v[24:25], v[84:85]
	v_pk_add_f32 v[24:25], v[24:25], v[84:85] neg_lo:[0,1] neg_hi:[0,1]
	v_mov_b32_e32 v72, v11
	v_pk_mul_f32 v[68:69], v[32:33], v[24:25] op_sel:[0,1] op_sel_hi:[0,0] neg_lo:[1,1] neg_hi:[1,0]
	v_pk_fma_f32 v[68:69], v[32:33], v[24:25], v[68:69] op_sel_hi:[0,1,1]
	v_pk_add_f32 v[24:25], v[44:45], v[86:87]
	v_pk_add_f32 v[44:45], v[44:45], v[86:87] neg_lo:[0,1] neg_hi:[0,1]
	v_lshl_add_u32 v13, v90, 3, 0
	v_xor_b32_e32 v71, 0x80000000, v44
	v_mov_b32_e32 v70, v45
	v_pk_add_f32 v[44:45], v[50:51], v[88:89]
	v_pk_add_f32 v[50:51], v[50:51], v[88:89] neg_lo:[0,1] neg_hi:[0,1]
	s_nop 0
	v_pk_mul_f32 v[82:83], v[32:33], v[50:51] op_sel:[0,1] op_sel_hi:[0,0] neg_lo:[1,1] neg_hi:[1,0]
	v_pk_fma_f32 v[82:83], v[32:33], v[50:51], v[82:83] op_sel_hi:[0,1,1] neg_lo:[1,0,0] neg_hi:[1,0,0]
	v_pk_add_f32 v[50:51], v[18:19], v[24:25]
	v_pk_add_f32 v[18:19], v[18:19], v[24:25] neg_lo:[0,1] neg_hi:[0,1]
	v_pk_add_f32 v[24:25], v[36:37], v[44:45]
	v_pk_add_f32 v[36:37], v[36:37], v[44:45] neg_lo:[0,1] neg_hi:[0,1]
	v_pk_add_f32 v[84:85], v[50:51], v[24:25]
	v_xor_b32_e32 v45, 0x80000000, v36
	v_mov_b32_e32 v44, v37
	v_pk_add_f32 v[36:37], v[50:51], v[24:25] neg_lo:[0,1] neg_hi:[0,1]
	v_pk_add_f32 v[50:51], v[18:19], v[44:45]
	v_pk_add_f32 v[24:25], v[18:19], v[44:45] neg_lo:[0,1] neg_hi:[0,1]
	v_pk_add_f32 v[44:45], v[68:69], v[82:83] neg_lo:[0,1] neg_hi:[0,1]
	v_pk_add_f32 v[18:19], v[28:29], v[70:71]
	v_pk_add_f32 v[70:71], v[28:29], v[70:71] neg_lo:[0,1] neg_hi:[0,1]
	v_pk_add_f32 v[28:29], v[68:69], v[82:83]
	v_xor_b32_e32 v69, 0x80000000, v44
	v_mov_b32_e32 v68, v45
	v_pk_add_f32 v[82:83], v[18:19], v[28:29]
	v_pk_add_f32 v[28:29], v[18:19], v[28:29] neg_lo:[0,1] neg_hi:[0,1]
	v_pk_add_f32 v[44:45], v[70:71], v[68:69]
	v_pk_add_f32 v[18:19], v[70:71], v[68:69] neg_lo:[0,1] neg_hi:[0,1]
	v_pk_add_f32 v[68:69], v[10:11], v[72:73]
	v_pk_add_f32 v[70:71], v[10:11], v[72:73] neg_lo:[0,1] neg_hi:[0,1]
	v_pk_add_f32 v[72:73], v[42:43], v[74:75]
	v_pk_add_f32 v[42:43], v[42:43], v[74:75] neg_lo:[0,1] neg_hi:[0,1]
	v_add_f32_e32 v10, v30, v31
	v_pk_mul_f32 v[74:75], v[38:39], v[42:43] op_sel:[0,1] op_sel_hi:[0,0] neg_lo:[1,1] neg_hi:[1,0]
	v_pk_fma_f32 v[42:43], v[34:35], v[42:43], v[74:75] op_sel_hi:[0,1,1]
	v_pk_add_f32 v[74:75], v[16:17], v[76:77]
	v_pk_add_f32 v[16:17], v[16:17], v[76:77] neg_lo:[0,1] neg_hi:[0,1]
	s_nop 0
	v_pk_mul_f32 v[76:77], v[32:33], v[16:17] op_sel:[0,1] op_sel_hi:[0,0] neg_lo:[1,1] neg_hi:[1,0]
	v_pk_fma_f32 v[16:17], v[32:33], v[16:17], v[76:77] op_sel_hi:[0,1,1]
	v_pk_add_f32 v[76:77], v[48:49], v[78:79]
	v_pk_add_f32 v[48:49], v[48:49], v[78:79] neg_lo:[0,1] neg_hi:[0,1]
	s_nop 0
	v_pk_mul_f32 v[78:79], v[34:35], v[48:49] op_sel:[0,1] op_sel_hi:[0,0] neg_lo:[1,1] neg_hi:[1,0]
	v_pk_fma_f32 v[78:79], v[38:39], v[48:49], v[78:79] op_sel_hi:[0,1,1]
	v_pk_add_f32 v[48:49], v[52:53], v[80:81]
	v_pk_add_f32 v[52:53], v[52:53], v[80:81] neg_lo:[0,1] neg_hi:[0,1]
	s_nop 0
	v_xor_b32_e32 v81, 0x80000000, v52
	v_mov_b32_e32 v80, v53
	v_pk_add_f32 v[52:53], v[54:55], v[62:63]
	v_pk_add_f32 v[54:55], v[54:55], v[62:63] neg_lo:[0,1] neg_hi:[0,1]
	s_nop 0
	v_pk_mul_f32 v[62:63], v[34:35], v[54:55] op_sel:[0,1] op_sel_hi:[0,0] neg_lo:[1,1] neg_hi:[1,0]
	v_pk_fma_f32 v[62:63], v[38:39], v[54:55], v[62:63] op_sel_hi:[0,1,1] neg_lo:[1,0,0] neg_hi:[1,0,0]
	v_pk_add_f32 v[54:55], v[58:59], v[64:65]
	v_pk_add_f32 v[58:59], v[58:59], v[64:65] neg_lo:[0,1] neg_hi:[0,1]
	s_nop 0
	v_pk_mul_f32 v[64:65], v[32:33], v[58:59] op_sel:[0,1] op_sel_hi:[0,0] neg_lo:[1,1] neg_hi:[1,0]
	v_pk_fma_f32 v[58:59], v[32:33], v[58:59], v[64:65] op_sel_hi:[0,1,1] neg_lo:[1,0,0] neg_hi:[1,0,0]
	v_pk_add_f32 v[64:65], v[56:57], v[66:67]
	v_pk_add_f32 v[56:57], v[56:57], v[66:67] neg_lo:[0,1] neg_hi:[0,1]
	s_nop 0
	v_pk_mul_f32 v[38:39], v[38:39], v[56:57] op_sel:[0,1] op_sel_hi:[0,0] neg_lo:[1,1] neg_hi:[1,0]
	v_pk_fma_f32 v[56:57], v[34:35], v[56:57], v[38:39] op_sel_hi:[0,1,1] neg_lo:[1,0,0] neg_hi:[1,0,0]
	v_pk_add_f32 v[38:39], v[52:53], v[72:73]
	v_pk_add_f32 v[52:53], v[72:73], v[52:53] neg_lo:[0,1] neg_hi:[0,1]
	v_pk_add_f32 v[34:35], v[68:69], v[48:49]
	v_pk_mul_f32 v[66:67], v[32:33], v[52:53] op_sel:[0,1] op_sel_hi:[0,0] neg_lo:[1,1] neg_hi:[1,0]
	v_pk_fma_f32 v[52:53], v[32:33], v[52:53], v[66:67] op_sel_hi:[0,1,1]
	v_pk_add_f32 v[66:67], v[74:75], v[54:55]
	v_pk_add_f32 v[54:55], v[74:75], v[54:55] neg_lo:[0,1] neg_hi:[0,1]
	v_pk_add_f32 v[48:49], v[68:69], v[48:49] neg_lo:[0,1] neg_hi:[0,1]
	v_xor_b32_e32 v69, 0x80000000, v54
	v_mov_b32_e32 v68, v55
	v_pk_add_f32 v[54:55], v[76:77], v[64:65]
	v_pk_add_f32 v[64:65], v[76:77], v[64:65] neg_lo:[0,1] neg_hi:[0,1]
	s_nop 0
	v_pk_mul_f32 v[72:73], v[32:33], v[64:65] op_sel:[0,1] op_sel_hi:[0,0] neg_lo:[1,1] neg_hi:[1,0]
	v_pk_fma_f32 v[64:65], v[32:33], v[64:65], v[72:73] op_sel_hi:[0,1,1] neg_lo:[1,0,0] neg_hi:[1,0,0]
	v_pk_add_f32 v[72:73], v[34:35], v[66:67]
	v_pk_add_f32 v[34:35], v[34:35], v[66:67] neg_lo:[0,1] neg_hi:[0,1]
	v_pk_add_f32 v[66:67], v[38:39], v[54:55]
	v_pk_add_f32 v[38:39], v[38:39], v[54:55] neg_lo:[0,1] neg_hi:[0,1]
	v_pk_add_f32 v[76:77], v[72:73], v[66:67]
	v_pk_add_f32 v[54:55], v[72:73], v[66:67] neg_lo:[0,1] neg_hi:[0,1]
	v_pk_add_f32 v[66:67], v[34:35], v[38:39] op_sel:[0,1] op_sel_hi:[1,0] neg_hi:[0,1]
	v_pk_add_f32 v[38:39], v[34:35], v[38:39] op_sel:[0,1] op_sel_hi:[1,0] neg_lo:[0,1]
	v_pk_add_f32 v[34:35], v[48:49], v[68:69]
	v_pk_add_f32 v[68:69], v[48:49], v[68:69] neg_lo:[0,1] neg_hi:[0,1]
	v_pk_add_f32 v[48:49], v[52:53], v[64:65]
	v_pk_add_f32 v[52:53], v[52:53], v[64:65] neg_lo:[0,1] neg_hi:[0,1]
	v_pk_add_f32 v[72:73], v[34:35], v[48:49]
	v_pk_add_f32 v[48:49], v[34:35], v[48:49] neg_lo:[0,1] neg_hi:[0,1]
	v_pk_add_f32 v[74:75], v[68:69], v[52:53] op_sel:[0,1] op_sel_hi:[1,0] neg_hi:[0,1]
	v_pk_add_f32 v[34:35], v[68:69], v[52:53] op_sel:[0,1] op_sel_hi:[1,0] neg_lo:[0,1]
	v_pk_add_f32 v[68:69], v[62:63], v[42:43]
	v_pk_add_f32 v[42:43], v[42:43], v[62:63] neg_lo:[0,1] neg_hi:[0,1]
	v_pk_add_f32 v[52:53], v[70:71], v[80:81]
	v_pk_mul_f32 v[62:63], v[32:33], v[42:43] op_sel:[0,1] op_sel_hi:[0,0] neg_lo:[1,1] neg_hi:[1,0]
	v_pk_fma_f32 v[62:63], v[32:33], v[42:43], v[62:63] op_sel_hi:[0,1,1]
	v_pk_add_f32 v[42:43], v[16:17], v[58:59]
	v_pk_add_f32 v[16:17], v[16:17], v[58:59] neg_lo:[0,1] neg_hi:[0,1]
	v_pk_add_f32 v[64:65], v[70:71], v[80:81] neg_lo:[0,1] neg_hi:[0,1]
	v_xor_b32_e32 v59, 0x80000000, v16
	v_mov_b32_e32 v58, v17
	v_pk_add_f32 v[16:17], v[78:79], v[56:57]
	v_pk_add_f32 v[56:57], v[78:79], v[56:57] neg_lo:[0,1] neg_hi:[0,1]
	s_nop 0
	v_pk_mul_f32 v[70:71], v[32:33], v[56:57] op_sel:[0,1] op_sel_hi:[0,0] neg_lo:[1,1] neg_hi:[1,0]
	v_pk_fma_f32 v[32:33], v[32:33], v[56:57], v[70:71] op_sel_hi:[0,1,1] neg_lo:[1,0,0] neg_hi:[1,0,0]
	v_pk_add_f32 v[56:57], v[52:53], v[42:43]
	v_pk_add_f32 v[42:43], v[52:53], v[42:43] neg_lo:[0,1] neg_hi:[0,1]
	v_pk_add_f32 v[52:53], v[68:69], v[16:17]
	v_pk_add_f32 v[16:17], v[68:69], v[16:17] neg_lo:[0,1] neg_hi:[0,1]
	v_pk_add_f32 v[70:71], v[56:57], v[52:53]
	v_xor_b32_e32 v69, 0x80000000, v16
	v_mov_b32_e32 v68, v17
	v_pk_add_f32 v[56:57], v[56:57], v[52:53] neg_lo:[0,1] neg_hi:[0,1]
	v_pk_add_f32 v[16:17], v[64:65], v[58:59]
	v_pk_add_f32 v[52:53], v[62:63], v[32:33]
	v_pk_add_f32 v[32:33], v[62:63], v[32:33] neg_lo:[0,1] neg_hi:[0,1]
	v_pk_add_f32 v[58:59], v[64:65], v[58:59] neg_lo:[0,1] neg_hi:[0,1]
	v_pk_add_f32 v[64:65], v[16:17], v[52:53]
	v_pk_add_f32 v[52:53], v[16:17], v[52:53] neg_lo:[0,1] neg_hi:[0,1]
	v_mov_b64_e32 v[16:17], s[90:91]
	v_pk_add_f32 v[78:79], v[42:43], v[68:69]
	v_pk_add_f32 v[42:43], v[42:43], v[68:69] neg_lo:[0,1] neg_hi:[0,1]
	v_pk_add_f32 v[68:69], v[58:59], v[32:33] op_sel:[0,1] op_sel_hi:[1,0] neg_hi:[0,1]
	v_pk_add_f32 v[32:33], v[58:59], v[32:33] op_sel:[0,1] op_sel_hi:[1,0] neg_lo:[0,1]
	v_pk_fma_f32 v[58:59], v[10:11], s[94:95], v[16:17] op_sel_hi:[0,1,1]
	ds_write_b64 v13, v[58:59]
	v_pk_fma_f32 v[58:59], v[178:179], s[90:91], v[178:179] op_sel:[1,0,0] op_sel_hi:[0,1,1]
	v_pk_mul_f32 v[62:63], v[58:59], v[76:77] op_sel:[1,1] op_sel_hi:[0,1] neg_lo:[0,1]
	v_pk_fma_f32 v[62:63], v[58:59], v[76:77], v[62:63] op_sel_hi:[1,0,1]
	ds_write_b64 v13, v[62:63] offset:4224
	v_pk_mul_f32 v[62:63], v[178:179], v[58:59] op_sel:[1,1] op_sel_hi:[0,1] neg_lo:[0,1]
	v_pk_fma_f32 v[58:59], v[178:179], v[58:59], v[62:63] op_sel_hi:[1,0,1]
	s_nop 0
	v_pk_mul_f32 v[62:63], v[58:59], v[84:85] op_sel:[1,1] op_sel_hi:[0,1] neg_lo:[0,1]
	v_pk_fma_f32 v[62:63], v[58:59], v[84:85], v[62:63] op_sel_hi:[1,0,1]
	ds_write_b64 v13, v[62:63] offset:8448
	v_pk_mul_f32 v[62:63], v[178:179], v[58:59] op_sel:[1,1] op_sel_hi:[0,1] neg_lo:[0,1]
	v_pk_fma_f32 v[58:59], v[178:179], v[58:59], v[62:63] op_sel_hi:[1,0,1]
	s_nop 0
	v_pk_mul_f32 v[62:63], v[58:59], v[70:71] op_sel:[1,1] op_sel_hi:[0,1] neg_lo:[0,1]
	v_pk_fma_f32 v[62:63], v[58:59], v[70:71], v[62:63] op_sel_hi:[1,0,1]
	ds_write_b64 v13, v[62:63] offset:12672
	v_pk_mul_f32 v[62:63], v[178:179], v[58:59] op_sel:[1,1] op_sel_hi:[0,1] neg_lo:[0,1]
	v_pk_fma_f32 v[58:59], v[178:179], v[58:59], v[62:63] op_sel_hi:[1,0,1]
	s_nop 0
	v_pk_mul_f32 v[62:63], v[60:61], v[58:59] op_sel:[1,1] op_sel_hi:[1,0] neg_lo:[1,0]
	s_nop 0
	v_pk_fma_f32 v[60:61], v[60:61], v[58:59], v[62:63] op_sel_hi:[0,1,1]
	ds_write_b64 v13, v[60:61] offset:16896
	v_pk_mul_f32 v[60:61], v[178:179], v[58:59] op_sel:[1,1] op_sel_hi:[0,1] neg_lo:[0,1]
	v_pk_fma_f32 v[58:59], v[178:179], v[58:59], v[60:61] op_sel_hi:[1,0,1]
	s_nop 0
	v_pk_mul_f32 v[60:61], v[58:59], v[72:73] op_sel:[1,1] op_sel_hi:[0,1] neg_lo:[0,1]
	v_pk_fma_f32 v[60:61], v[58:59], v[72:73], v[60:61] op_sel_hi:[1,0,1]
	ds_write_b64 v13, v[60:61] offset:21120
	v_pk_mul_f32 v[60:61], v[178:179], v[58:59] op_sel:[1,1] op_sel_hi:[0,1] neg_lo:[0,1]
	v_pk_fma_f32 v[58:59], v[178:179], v[58:59], v[60:61] op_sel_hi:[1,0,1]
	s_nop 0
	v_pk_mul_f32 v[60:61], v[82:83], v[58:59] op_sel:[1,1] op_sel_hi:[1,0] neg_lo:[1,0]
	s_nop 0
	v_pk_fma_f32 v[60:61], v[82:83], v[58:59], v[60:61] op_sel_hi:[0,1,1]
	ds_write_b64 v13, v[60:61] offset:25344
	v_pk_mul_f32 v[60:61], v[178:179], v[58:59] op_sel:[1,1] op_sel_hi:[0,1] neg_lo:[0,1]
	v_pk_fma_f32 v[58:59], v[178:179], v[58:59], v[60:61] op_sel_hi:[1,0,1]
	s_nop 0
	v_pk_mul_f32 v[60:61], v[64:65], v[58:59] op_sel:[1,1] op_sel_hi:[1,0] neg_lo:[1,0]
	s_nop 0
	v_pk_fma_f32 v[60:61], v[64:65], v[58:59], v[60:61] op_sel_hi:[0,1,1]
	ds_write_b64 v13, v[60:61] offset:29568
	v_pk_mul_f32 v[60:61], v[178:179], v[58:59] op_sel:[1,1] op_sel_hi:[0,1] neg_lo:[0,1]
	v_pk_fma_f32 v[58:59], v[178:179], v[58:59], v[60:61] op_sel_hi:[1,0,1]
	s_nop 0
	v_pk_mul_f32 v[60:61], v[46:47], v[58:59] op_sel:[1,1] op_sel_hi:[1,0] neg_lo:[1,0]
	s_nop 0
	v_pk_fma_f32 v[46:47], v[46:47], v[58:59], v[60:61] op_sel_hi:[0,1,1]
	ds_write_b64 v13, v[46:47] offset:33792
	v_pk_mul_f32 v[46:47], v[178:179], v[58:59] op_sel:[1,1] op_sel_hi:[0,1] neg_lo:[0,1]
	v_pk_fma_f32 v[46:47], v[178:179], v[58:59], v[46:47] op_sel_hi:[1,0,1]
	s_nop 0
	v_pk_mul_f32 v[58:59], v[66:67], v[46:47] op_sel:[1,1] op_sel_hi:[1,0] neg_lo:[1,0]
	s_nop 0
	v_pk_fma_f32 v[58:59], v[66:67], v[46:47], v[58:59] op_sel_hi:[0,1,1]
	ds_write_b64 v13, v[58:59] offset:38016
	v_pk_mul_f32 v[58:59], v[178:179], v[46:47] op_sel:[1,1] op_sel_hi:[0,1] neg_lo:[0,1]
	v_pk_fma_f32 v[46:47], v[178:179], v[46:47], v[58:59] op_sel_hi:[1,0,1]
	s_nop 0
	v_pk_mul_f32 v[58:59], v[50:51], v[46:47] op_sel:[1,1] op_sel_hi:[1,0] neg_lo:[1,0]
	s_nop 0
	v_pk_fma_f32 v[50:51], v[50:51], v[46:47], v[58:59] op_sel_hi:[0,1,1]
	ds_write_b64 v13, v[50:51] offset:42240
	v_pk_mul_f32 v[50:51], v[178:179], v[46:47] op_sel:[1,1] op_sel_hi:[0,1] neg_lo:[0,1]
	v_pk_fma_f32 v[46:47], v[178:179], v[46:47], v[50:51] op_sel_hi:[1,0,1]
	s_nop 0
	v_pk_mul_f32 v[50:51], v[78:79], v[46:47] op_sel:[1,1] op_sel_hi:[1,0] neg_lo:[1,0]
	s_nop 0
	v_pk_fma_f32 v[50:51], v[78:79], v[46:47], v[50:51] op_sel_hi:[0,1,1]
	ds_write_b64 v13, v[50:51] offset:46464
	v_pk_mul_f32 v[50:51], v[178:179], v[46:47] op_sel:[1,1] op_sel_hi:[0,1] neg_lo:[0,1]
	v_pk_fma_f32 v[46:47], v[178:179], v[46:47], v[50:51] op_sel_hi:[1,0,1]
	s_nop 0
	v_pk_mul_f32 v[50:51], v[40:41], v[46:47] op_sel:[1,1] op_sel_hi:[1,0] neg_lo:[1,0]
	s_nop 0
	v_pk_fma_f32 v[40:41], v[40:41], v[46:47], v[50:51] op_sel_hi:[0,1,1]
	ds_write_b64 v13, v[40:41] offset:50688
	v_pk_mul_f32 v[40:41], v[178:179], v[46:47] op_sel:[1,1] op_sel_hi:[0,1] neg_lo:[0,1]
	v_pk_fma_f32 v[40:41], v[178:179], v[46:47], v[40:41] op_sel_hi:[1,0,1]
	s_nop 0
	v_pk_mul_f32 v[46:47], v[74:75], v[40:41] op_sel:[1,1] op_sel_hi:[1,0] neg_lo:[1,0]
	s_nop 0
	v_pk_fma_f32 v[46:47], v[74:75], v[40:41], v[46:47] op_sel_hi:[0,1,1]
	ds_write_b64 v13, v[46:47] offset:54912
	v_pk_mul_f32 v[46:47], v[178:179], v[40:41] op_sel:[1,1] op_sel_hi:[0,1] neg_lo:[0,1]
	v_pk_fma_f32 v[40:41], v[178:179], v[40:41], v[46:47] op_sel_hi:[1,0,1]
	s_nop 0
	v_pk_mul_f32 v[46:47], v[44:45], v[40:41] op_sel:[1,1] op_sel_hi:[1,0] neg_lo:[1,0]
	s_nop 0
	v_pk_fma_f32 v[44:45], v[44:45], v[40:41], v[46:47] op_sel_hi:[0,1,1]
	ds_write_b64 v13, v[44:45] offset:59136
	v_pk_mul_f32 v[44:45], v[178:179], v[40:41] op_sel:[1,1] op_sel_hi:[0,1] neg_lo:[0,1]
	v_pk_fma_f32 v[40:41], v[178:179], v[40:41], v[44:45] op_sel_hi:[1,0,1]
	s_nop 0
	v_pk_mul_f32 v[44:45], v[68:69], v[40:41] op_sel:[1,1] op_sel_hi:[1,0] neg_lo:[1,0]
	s_nop 0
	v_pk_fma_f32 v[44:45], v[68:69], v[40:41], v[44:45] op_sel_hi:[0,1,1]
	ds_write_b64 v13, v[44:45] offset:63360
	v_pk_mul_f32 v[44:45], v[178:179], v[40:41] op_sel:[1,1] op_sel_hi:[0,1] neg_lo:[0,1]
	v_pk_fma_f32 v[40:41], v[178:179], v[40:41], v[44:45] op_sel_hi:[1,0,1]
	s_mov_b32 s44, s95
	v_sub_f32_e32 v10, v30, v31
	v_pk_mul_f32 v[30:31], v[40:41], s[44:45]
	s_nop 0
	v_pk_fma_f32 v[30:31], v[10:11], v[40:41], v[30:31] op_sel:[0,0,1] op_sel_hi:[0,1,0]
	v_add_u32_e32 v10, 0x10800, v13
	ds_write_b64 v10, v[30:31]
	v_pk_mul_f32 v[30:31], v[178:179], v[40:41] op_sel:[1,1] op_sel_hi:[0,1] neg_lo:[0,1]
	v_pk_fma_f32 v[30:31], v[178:179], v[40:41], v[30:31] op_sel_hi:[1,0,1]
	s_nop 0
	v_pk_mul_f32 v[40:41], v[54:55], v[30:31] op_sel:[1,1] op_sel_hi:[1,0] neg_lo:[1,0]
	v_add_u32_e32 v10, 0x11880, v13
	v_pk_fma_f32 v[40:41], v[54:55], v[30:31], v[40:41] op_sel_hi:[0,1,1]
	ds_write_b64 v10, v[40:41]
	v_pk_mul_f32 v[40:41], v[178:179], v[30:31] op_sel:[1,1] op_sel_hi:[0,1] neg_lo:[0,1]
	v_pk_fma_f32 v[30:31], v[178:179], v[30:31], v[40:41] op_sel_hi:[1,0,1]
	s_nop 0
	v_pk_mul_f32 v[40:41], v[36:37], v[30:31] op_sel:[1,1] op_sel_hi:[1,0] neg_lo:[1,0]
	v_add_u32_e32 v10, 0x12900, v13
	v_pk_fma_f32 v[36:37], v[36:37], v[30:31], v[40:41] op_sel_hi:[0,1,1]
	ds_write_b64 v10, v[36:37]
	v_pk_mul_f32 v[36:37], v[178:179], v[30:31] op_sel:[1,1] op_sel_hi:[0,1] neg_lo:[0,1]
	v_pk_fma_f32 v[30:31], v[178:179], v[30:31], v[36:37] op_sel_hi:[1,0,1]
	s_nop 0
	v_pk_mul_f32 v[36:37], v[56:57], v[30:31] op_sel:[1,1] op_sel_hi:[1,0] neg_lo:[1,0]
	v_add_u32_e32 v10, 0x13980, v13
	v_pk_fma_f32 v[36:37], v[56:57], v[30:31], v[36:37] op_sel_hi:[0,1,1]
	ds_write_b64 v10, v[36:37]
	v_pk_mul_f32 v[36:37], v[178:179], v[30:31] op_sel:[1,1] op_sel_hi:[0,1] neg_lo:[0,1]
	v_pk_fma_f32 v[30:31], v[178:179], v[30:31], v[36:37] op_sel_hi:[1,0,1]
	s_nop 0
	v_pk_mul_f32 v[36:37], v[26:27], v[30:31] op_sel:[1,1] op_sel_hi:[1,0] neg_lo:[1,0]
	v_add_u32_e32 v10, 0x14a00, v13
	v_pk_fma_f32 v[26:27], v[26:27], v[30:31], v[36:37] op_sel_hi:[0,1,1]
	ds_write_b64 v10, v[26:27]
	v_pk_mul_f32 v[26:27], v[178:179], v[30:31] op_sel:[1,1] op_sel_hi:[0,1] neg_lo:[0,1]
	v_pk_fma_f32 v[26:27], v[178:179], v[30:31], v[26:27] op_sel_hi:[1,0,1]
	s_nop 0
	v_pk_mul_f32 v[30:31], v[48:49], v[26:27] op_sel:[1,1] op_sel_hi:[1,0] neg_lo:[1,0]
	v_add_u32_e32 v10, 0x15a80, v13
	v_pk_fma_f32 v[30:31], v[48:49], v[26:27], v[30:31] op_sel_hi:[0,1,1]
	ds_write_b64 v10, v[30:31]
	v_pk_mul_f32 v[30:31], v[178:179], v[26:27] op_sel:[1,1] op_sel_hi:[0,1] neg_lo:[0,1]
	v_pk_fma_f32 v[26:27], v[178:179], v[26:27], v[30:31] op_sel_hi:[1,0,1]
	s_nop 0
	v_pk_mul_f32 v[30:31], v[28:29], v[26:27] op_sel:[1,1] op_sel_hi:[1,0] neg_lo:[1,0]
	v_add_u32_e32 v10, 0x16b00, v13
	v_pk_fma_f32 v[28:29], v[28:29], v[26:27], v[30:31] op_sel_hi:[0,1,1]
	ds_write_b64 v10, v[28:29]
	v_pk_mul_f32 v[28:29], v[178:179], v[26:27] op_sel:[1,1] op_sel_hi:[0,1] neg_lo:[0,1]
	v_pk_fma_f32 v[26:27], v[178:179], v[26:27], v[28:29] op_sel_hi:[1,0,1]
	s_nop 0
	v_pk_mul_f32 v[28:29], v[52:53], v[26:27] op_sel:[1,1] op_sel_hi:[1,0] neg_lo:[1,0]
	v_add_u32_e32 v10, 0x17b80, v13
	v_pk_fma_f32 v[28:29], v[52:53], v[26:27], v[28:29] op_sel_hi:[0,1,1]
	ds_write_b64 v10, v[28:29]
	v_pk_mul_f32 v[28:29], v[178:179], v[26:27] op_sel:[1,1] op_sel_hi:[0,1] neg_lo:[0,1]
	v_pk_fma_f32 v[26:27], v[178:179], v[26:27], v[28:29] op_sel_hi:[1,0,1]
	s_nop 0
	v_pk_mul_f32 v[28:29], v[20:21], v[26:27] op_sel:[1,1] op_sel_hi:[1,0] neg_lo:[1,0]
	v_add_u32_e32 v10, 0x18c00, v13
	v_pk_fma_f32 v[20:21], v[20:21], v[26:27], v[28:29] op_sel_hi:[0,1,1]
	ds_write_b64 v10, v[20:21]
	v_pk_mul_f32 v[20:21], v[178:179], v[26:27] op_sel:[1,1] op_sel_hi:[0,1] neg_lo:[0,1]
	v_pk_fma_f32 v[20:21], v[178:179], v[26:27], v[20:21] op_sel_hi:[1,0,1]
	s_nop 0
	v_pk_mul_f32 v[26:27], v[38:39], v[20:21] op_sel:[1,1] op_sel_hi:[1,0] neg_lo:[1,0]
	v_add_u32_e32 v10, 0x19c80, v13
	v_pk_fma_f32 v[26:27], v[38:39], v[20:21], v[26:27] op_sel_hi:[0,1,1]
	ds_write_b64 v10, v[26:27]
	v_pk_mul_f32 v[26:27], v[178:179], v[20:21] op_sel:[1,1] op_sel_hi:[0,1] neg_lo:[0,1]
	v_pk_fma_f32 v[20:21], v[178:179], v[20:21], v[26:27] op_sel_hi:[1,0,1]
	s_nop 0
	v_pk_mul_f32 v[26:27], v[24:25], v[20:21] op_sel:[1,1] op_sel_hi:[1,0] neg_lo:[1,0]
	v_add_u32_e32 v10, 0x1ad00, v13
	v_pk_fma_f32 v[24:25], v[24:25], v[20:21], v[26:27] op_sel_hi:[0,1,1]
	ds_write_b64 v10, v[24:25]
	v_pk_mul_f32 v[24:25], v[178:179], v[20:21] op_sel:[1,1] op_sel_hi:[0,1] neg_lo:[0,1]
	v_pk_fma_f32 v[20:21], v[178:179], v[20:21], v[24:25] op_sel_hi:[1,0,1]
	s_nop 0
	v_pk_mul_f32 v[24:25], v[42:43], v[20:21] op_sel:[1,1] op_sel_hi:[1,0] neg_lo:[1,0]
	v_add_u32_e32 v10, 0x1bd80, v13
	v_pk_fma_f32 v[24:25], v[42:43], v[20:21], v[24:25] op_sel_hi:[0,1,1]
	ds_write_b64 v10, v[24:25]
	v_pk_mul_f32 v[24:25], v[178:179], v[20:21] op_sel:[1,1] op_sel_hi:[0,1] neg_lo:[0,1]
	v_pk_fma_f32 v[20:21], v[178:179], v[20:21], v[24:25] op_sel_hi:[1,0,1]
	s_nop 0
	v_pk_mul_f32 v[24:25], v[14:15], v[20:21] op_sel:[1,1] op_sel_hi:[1,0] neg_lo:[1,0]
	v_add_u32_e32 v10, 0x1ce00, v13
	v_pk_fma_f32 v[14:15], v[14:15], v[20:21], v[24:25] op_sel_hi:[0,1,1]
	ds_write_b64 v10, v[14:15]
	v_pk_mul_f32 v[14:15], v[178:179], v[20:21] op_sel:[1,1] op_sel_hi:[0,1] neg_lo:[0,1]
	v_pk_fma_f32 v[14:15], v[178:179], v[20:21], v[14:15] op_sel_hi:[1,0,1]
	s_nop 0
	v_pk_mul_f32 v[20:21], v[34:35], v[14:15] op_sel:[1,1] op_sel_hi:[1,0] neg_lo:[1,0]
	v_add_u32_e32 v10, 0x1de80, v13
	v_pk_fma_f32 v[20:21], v[34:35], v[14:15], v[20:21] op_sel_hi:[0,1,1]
	ds_write_b64 v10, v[20:21]
	v_pk_mul_f32 v[20:21], v[178:179], v[14:15] op_sel:[1,1] op_sel_hi:[0,1] neg_lo:[0,1]
	v_pk_fma_f32 v[14:15], v[178:179], v[14:15], v[20:21] op_sel_hi:[1,0,1]
	s_nop 0
	v_pk_mul_f32 v[20:21], v[18:19], v[14:15] op_sel:[1,1] op_sel_hi:[1,0] neg_lo:[1,0]
	v_add_u32_e32 v10, 0x1ef00, v13
	v_pk_fma_f32 v[18:19], v[18:19], v[14:15], v[20:21] op_sel_hi:[0,1,1]
	ds_write_b64 v10, v[18:19]
	v_pk_mul_f32 v[18:19], v[178:179], v[14:15] op_sel:[1,1] op_sel_hi:[0,1] neg_lo:[0,1]
	v_pk_fma_f32 v[14:15], v[178:179], v[14:15], v[18:19] op_sel_hi:[1,0,1]
	s_nop 0
	v_pk_mul_f32 v[18:19], v[32:33], v[14:15] op_sel:[1,1] op_sel_hi:[1,0] neg_lo:[1,0]
	v_add_u32_e32 v10, 0x1ff80, v13
	v_pk_fma_f32 v[14:15], v[32:33], v[14:15], v[18:19] op_sel_hi:[0,1,1]
	ds_write_b64 v10, v[14:15]
	v_mov_b32_e32 v10, v174
	v_mov_b32_e32 v13, v172
	s_waitcnt lgkmcnt(0)
	s_barrier
	v_mov_b32_e32 v14, v180
	v_xad_u32 v30, v13, 3, v10
	v_lshl_add_u32 v73, v30, 3, 0
	v_xad_u32 v30, v13, 4, v10
	v_lshl_add_u32 v72, v30, 3, 0
	v_xad_u32 v30, v13, 5, v10
	v_lshl_add_u32 v71, v30, 3, 0
	v_xad_u32 v30, v13, 6, v10
	v_lshl_add_u32 v70, v30, 3, 0
	v_xad_u32 v30, v13, 7, v10
	v_lshl_add_u32 v69, v30, 3, 0
	v_xad_u32 v30, v13, 8, v10
	v_lshl_add_u32 v30, v30, 3, 0
	v_add_u32_e32 v68, 0x800, v30
	v_xad_u32 v30, v13, 9, v10
	v_lshl_add_u32 v30, v30, 3, 0
	v_add_u32_e32 v67, 0x800, v30
	v_xad_u32 v30, v13, 10, v10
	v_lshl_add_u32 v30, v30, 3, 0
	v_add_u32_e32 v66, 0x800, v30
	v_xad_u32 v30, v13, 11, v10
	v_lshl_add_u32 v30, v30, 3, 0
	v_add_u32_e32 v18, v13, v10
	v_add_u32_e32 v65, 0x800, v30
	v_xad_u32 v30, v13, 12, v10
	v_mov_b32_e32 v15, v181
	v_lshl_add_u32 v76, v18, 3, 0
	v_lshl_add_u32 v30, v30, 3, 0
	ds_read2_b64 v[18:21], v76 offset1:16
	ds_read2_b64 v[40:43], v68 offset1:16
	v_add_u32_e32 v64, 0x800, v30
	v_xad_u32 v30, v13, 13, v10
	v_xad_u32 v22, v13, 1, v10
	v_lshl_add_u32 v30, v30, 3, 0
	v_lshl_add_u32 v75, v22, 3, 0
	v_xad_u32 v26, v13, 2, v10
	v_add_u32_e32 v63, 0x800, v30
	v_xad_u32 v30, v13, 14, v10
	v_xad_u32 v10, v13, 15, v10
	ds_read2_b64 v[22:25], v75 offset0:32 offset1:48
	ds_read2_b64 v[48:51], v67 offset0:32 offset1:48
	v_lshl_add_u32 v30, v30, 3, 0
	v_lshl_add_u32 v10, v10, 3, 0
	v_lshl_add_u32 v74, v26, 3, 0
	v_add_u32_e32 v62, 0x800, v30
	v_add_u32_e32 v13, 0x800, v10
	ds_read2_b64 v[26:29], v74 offset0:64 offset1:80
	ds_read2_b64 v[58:61], v73 offset0:96 offset1:112
	ds_read2_b64 v[78:81], v72 offset0:128 offset1:144
	ds_read2_b64 v[82:85], v71 offset0:160 offset1:176
	ds_read2_b64 v[86:89], v70 offset0:192 offset1:208
	ds_read2_b64 v[90:93], v69 offset0:224 offset1:240
	ds_read2_b64 v[54:57], v66 offset0:64 offset1:80
	ds_read2_b64 v[94:97], v65 offset0:96 offset1:112
	ds_read2_b64 v[98:101], v64 offset0:128 offset1:144
	ds_read2_b64 v[102:105], v63 offset0:160 offset1:176
	ds_read2_b64 v[106:109], v62 offset0:192 offset1:208
	ds_read2_b64 v[110:113], v13 offset0:224 offset1:240
	s_waitcnt lgkmcnt(14)
	v_pk_add_f32 v[114:115], v[18:19], v[40:41]
	v_pk_add_f32 v[40:41], v[18:19], v[40:41] neg_lo:[0,1] neg_hi:[0,1]
	v_pk_add_f32 v[18:19], v[20:21], v[42:43]
	v_pk_add_f32 v[20:21], v[20:21], v[42:43] neg_lo:[0,1] neg_hi:[0,1]
	v_mov_b32_e32 v30, v164
	v_mov_b32_e32 v32, v165
	v_mov_b32_e32 v34, v166
	v_mov_b32_e32 v10, v167
	v_mov_b32_e32 v38, v168
	v_mov_b32_e32 v36, v169
	v_mov_b32_e32 v46, v170
	v_mov_b32_e32 v31, v171
	v_pk_mul_f32 v[42:43], v[20:21], v[46:47] op_sel:[1,0] op_sel_hi:[0,0] neg_lo:[1,1] neg_hi:[0,1]
	s_mov_b32 s14, s95
	v_pk_fma_f32 v[44:45], v[20:21], v[30:31], v[42:43] op_sel_hi:[1,0,1]
	s_waitcnt lgkmcnt(12)
	v_pk_add_f32 v[20:21], v[22:23], v[48:49]
	v_pk_add_f32 v[22:23], v[22:23], v[48:49] neg_lo:[0,1] neg_hi:[0,1]
	s_mov_b32 s15, s94
	v_pk_mul_f32 v[42:43], v[22:23], v[36:37] op_sel:[1,0] op_sel_hi:[0,0] neg_lo:[1,1] neg_hi:[0,1]
	s_nop 0
	v_pk_fma_f32 v[48:49], v[22:23], v[32:33], v[42:43] op_sel_hi:[1,0,1]
	v_pk_add_f32 v[22:23], v[24:25], v[50:51]
	v_pk_add_f32 v[24:25], v[24:25], v[50:51] neg_lo:[0,1] neg_hi:[0,1]
	s_nop 0
	v_pk_mul_f32 v[42:43], v[24:25], v[38:39] op_sel:[1,0] op_sel_hi:[0,0] neg_lo:[1,1] neg_hi:[0,1]
	s_nop 0
	v_pk_fma_f32 v[52:53], v[24:25], v[34:35], v[42:43] op_sel_hi:[1,0,1]
	s_waitcnt lgkmcnt(5)
	v_pk_add_f32 v[24:25], v[26:27], v[54:55]
	v_pk_add_f32 v[26:27], v[26:27], v[54:55] neg_lo:[0,1] neg_hi:[0,1]
	s_nop 0
	v_pk_mul_f32 v[42:43], v[26:27], v[10:11] op_sel:[1,0] op_sel_hi:[0,0] neg_lo:[1,1] neg_hi:[0,1]
	s_nop 0
	v_pk_fma_f32 v[54:55], v[26:27], v[10:11], v[42:43] op_sel_hi:[1,0,1]
	v_pk_add_f32 v[26:27], v[28:29], v[56:57]
	v_pk_add_f32 v[28:29], v[28:29], v[56:57] neg_lo:[0,1] neg_hi:[0,1]
	s_nop 0
	v_pk_mul_f32 v[42:43], v[28:29], v[38:39] op_sel_hi:[1,0]
	s_nop 0
	v_pk_fma_f32 v[56:57], v[28:29], v[34:35], v[42:43] op_sel:[1,0,0] op_sel_hi:[0,0,1] neg_lo:[1,1,0] neg_hi:[0,1,0]
	s_waitcnt lgkmcnt(4)
	v_pk_add_f32 v[42:43], v[58:59], v[94:95] neg_lo:[0,1] neg_hi:[0,1]
	v_pk_add_f32 v[28:29], v[58:59], v[94:95]
	v_pk_mul_f32 v[50:51], v[42:43], v[36:37] op_sel_hi:[1,0]
	s_nop 0
	v_pk_fma_f32 v[58:59], v[42:43], v[32:33], v[50:51] op_sel:[1,0,0] op_sel_hi:[0,0,1] neg_lo:[1,1,0] neg_hi:[0,1,0]
	v_pk_add_f32 v[50:51], v[60:61], v[96:97] neg_lo:[0,1] neg_hi:[0,1]
	v_pk_add_f32 v[42:43], v[60:61], v[96:97]
	v_pk_mul_f32 v[60:61], v[50:51], v[46:47] op_sel_hi:[1,0]
	v_xor_b32_e32 v94, 0x80000000, v51
	v_mov_b32_e32 v95, v50
	s_waitcnt lgkmcnt(3)
	v_pk_add_f32 v[50:51], v[78:79], v[98:99]
	v_pk_add_f32 v[78:79], v[78:79], v[98:99] neg_lo:[0,1] neg_hi:[0,1]
	v_pk_fma_f32 v[60:61], v[94:95], v[30:31], v[60:61] op_sel_hi:[1,0,1] neg_lo:[0,1,0] neg_hi:[0,1,0]
	v_xor_b32_e32 v95, 0x80000000, v78
	v_mov_b32_e32 v94, v79
	v_pk_add_f32 v[78:79], v[80:81], v[100:101]
	v_pk_add_f32 v[80:81], v[80:81], v[100:101] neg_lo:[0,1] neg_hi:[0,1]
	s_nop 0
	v_pk_mul_f32 v[96:97], v[80:81], v[46:47] op_sel_hi:[1,0] neg_lo:[0,1] neg_hi:[0,1]
	s_nop 0
	v_pk_fma_f32 v[80:81], v[80:81], v[30:31], v[96:97] op_sel:[1,0,0] op_sel_hi:[0,0,1] neg_lo:[1,1,0] neg_hi:[0,1,0]
	s_waitcnt lgkmcnt(2)
	v_pk_add_f32 v[96:97], v[82:83], v[102:103]
	v_pk_add_f32 v[82:83], v[82:83], v[102:103] neg_lo:[0,1] neg_hi:[0,1]
	s_nop 0
	v_pk_mul_f32 v[98:99], v[82:83], v[36:37] op_sel_hi:[1,0] neg_lo:[0,1] neg_hi:[0,1]
	s_nop 0
	v_pk_fma_f32 v[82:83], v[82:83], v[32:33], v[98:99] op_sel:[1,0,0] op_sel_hi:[0,0,1] neg_lo:[1,1,0] neg_hi:[0,1,0]
	v_pk_add_f32 v[98:99], v[84:85], v[104:105]
	v_pk_add_f32 v[84:85], v[84:85], v[104:105] neg_lo:[0,1] neg_hi:[0,1]
	s_nop 0
	v_pk_mul_f32 v[100:101], v[84:85], v[38:39] op_sel_hi:[1,0] neg_lo:[0,1] neg_hi:[0,1]
	s_nop 0
	v_pk_fma_f32 v[84:85], v[84:85], v[34:35], v[100:101] op_sel:[1,0,0] op_sel_hi:[0,0,1] neg_lo:[1,1,0] neg_hi:[0,1,0]
	s_waitcnt lgkmcnt(1)
	v_pk_add_f32 v[100:101], v[86:87], v[106:107]
	v_pk_add_f32 v[86:87], v[86:87], v[106:107] neg_lo:[0,1] neg_hi:[0,1]
	s_nop 0
	v_pk_mul_f32 v[102:103], v[86:87], v[10:11] op_sel:[1,0] op_sel_hi:[0,0] neg_lo:[1,1] neg_hi:[0,1]
	s_nop 0
	v_pk_fma_f32 v[86:87], v[86:87], v[10:11], v[102:103] op_sel_hi:[1,0,1] neg_lo:[0,1,0] neg_hi:[0,1,0]
	v_pk_add_f32 v[102:103], v[88:89], v[108:109]
	v_pk_add_f32 v[88:89], v[88:89], v[108:109] neg_lo:[0,1] neg_hi:[0,1]
	s_nop 0
	v_pk_mul_f32 v[38:39], v[88:89], v[38:39] op_sel:[1,0] op_sel_hi:[0,0] neg_lo:[1,1] neg_hi:[0,1]
	s_nop 0
	v_pk_fma_f32 v[88:89], v[88:89], v[34:35], v[38:39] op_sel_hi:[1,0,1] neg_lo:[0,1,0] neg_hi:[0,1,0]
	s_waitcnt lgkmcnt(0)
	v_pk_add_f32 v[38:39], v[90:91], v[110:111] neg_lo:[0,1] neg_hi:[0,1]
	v_pk_add_f32 v[34:35], v[90:91], v[110:111]
	v_pk_mul_f32 v[90:91], v[38:39], v[36:37] op_sel:[1,0] op_sel_hi:[0,0] neg_lo:[1,1] neg_hi:[0,1]
	s_nop 0
	v_pk_fma_f32 v[90:91], v[38:39], v[32:33], v[90:91] op_sel_hi:[1,0,1] neg_lo:[0,1,0] neg_hi:[0,1,0]
	v_pk_add_f32 v[38:39], v[92:93], v[112:113]
	v_pk_add_f32 v[92:93], v[92:93], v[112:113] neg_lo:[0,1] neg_hi:[0,1]
	s_nop 0
	v_pk_mul_f32 v[46:47], v[92:93], v[46:47] op_sel:[1,0] op_sel_hi:[0,0] neg_lo:[1,1] neg_hi:[0,1]
	s_nop 0
	v_pk_fma_f32 v[92:93], v[92:93], v[30:31], v[46:47] op_sel_hi:[1,0,1] neg_lo:[0,1,0] neg_hi:[0,1,0]
	v_pk_add_f32 v[46:47], v[18:19], v[78:79]
	v_pk_add_f32 v[18:19], v[18:19], v[78:79] neg_lo:[0,1] neg_hi:[0,1]
	v_pk_add_f32 v[30:31], v[114:115], v[50:51]
	v_pk_mul_f32 v[78:79], v[18:19], v[36:37] op_sel:[1,0] op_sel_hi:[0,0] neg_lo:[1,1] neg_hi:[0,1]
	v_pk_add_f32 v[50:51], v[114:115], v[50:51] neg_lo:[0,1] neg_hi:[0,1]
	v_pk_fma_f32 v[78:79], v[18:19], v[32:33], v[78:79] op_sel_hi:[1,0,1]
	v_pk_add_f32 v[18:19], v[20:21], v[96:97]
	v_pk_add_f32 v[20:21], v[20:21], v[96:97] neg_lo:[0,1] neg_hi:[0,1]
	s_nop 0
	v_pk_mul_f32 v[96:97], v[20:21], v[10:11] op_sel:[1,0] op_sel_hi:[0,0] neg_lo:[1,1] neg_hi:[0,1]
	s_nop 0
	v_pk_fma_f32 v[20:21], v[20:21], v[10:11], v[96:97] op_sel_hi:[1,0,1]
	v_pk_add_f32 v[96:97], v[22:23], v[98:99]
	v_pk_add_f32 v[22:23], v[22:23], v[98:99] neg_lo:[0,1] neg_hi:[0,1]
	s_nop 0
	v_pk_mul_f32 v[98:99], v[22:23], v[36:37] op_sel_hi:[1,0]
	v_xor_b32_e32 v104, 0x80000000, v23
	v_mov_b32_e32 v105, v22
	v_pk_add_f32 v[22:23], v[24:25], v[100:101]
	v_pk_add_f32 v[24:25], v[24:25], v[100:101] neg_lo:[0,1] neg_hi:[0,1]
	v_pk_fma_f32 v[98:99], v[104:105], v[32:33], v[98:99] op_sel_hi:[1,0,1] neg_lo:[0,1,0] neg_hi:[0,1,0]
	v_xor_b32_e32 v101, 0x80000000, v24
	v_mov_b32_e32 v100, v25
	v_pk_add_f32 v[24:25], v[26:27], v[102:103]
	v_pk_add_f32 v[26:27], v[26:27], v[102:103] neg_lo:[0,1] neg_hi:[0,1]
	s_nop 0
	v_pk_mul_f32 v[102:103], v[26:27], v[36:37] op_sel_hi:[1,0] neg_lo:[0,1] neg_hi:[0,1]
	v_xor_b32_e32 v104, 0x80000000, v27
	v_mov_b32_e32 v105, v26
	v_pk_add_f32 v[26:27], v[28:29], v[34:35]
	v_pk_add_f32 v[28:29], v[28:29], v[34:35] neg_lo:[0,1] neg_hi:[0,1]
	v_pk_fma_f32 v[102:103], v[104:105], v[32:33], v[102:103] op_sel_hi:[1,0,1] neg_lo:[0,1,0] neg_hi:[0,1,0]
	v_pk_mul_f32 v[34:35], v[28:29], v[10:11] op_sel:[1,0] op_sel_hi:[0,0] neg_lo:[1,1] neg_hi:[0,1]
	v_pk_add_f32 v[104:105], v[30:31], v[22:23] neg_lo:[0,1] neg_hi:[0,1]
	v_pk_fma_f32 v[28:29], v[28:29], v[10:11], v[34:35] op_sel_hi:[1,0,1] neg_lo:[0,1,0] neg_hi:[0,1,0]
	v_pk_add_f32 v[34:35], v[42:43], v[38:39]
	v_pk_add_f32 v[38:39], v[42:43], v[38:39] neg_lo:[0,1] neg_hi:[0,1]
	s_nop 0
	v_pk_mul_f32 v[42:43], v[38:39], v[36:37] op_sel:[1,0] op_sel_hi:[0,0] neg_lo:[1,1] neg_hi:[0,1]
	s_nop 0
	v_pk_fma_f32 v[42:43], v[38:39], v[32:33], v[42:43] op_sel_hi:[1,0,1] neg_lo:[0,1,0] neg_hi:[0,1,0]
	v_pk_add_f32 v[38:39], v[30:31], v[22:23]
	v_pk_add_f32 v[22:23], v[46:47], v[24:25]
	v_pk_add_f32 v[24:25], v[46:47], v[24:25] neg_lo:[0,1] neg_hi:[0,1]
	s_nop 0
	v_pk_mul_f32 v[30:31], v[24:25], v[10:11] op_sel:[1,0] op_sel_hi:[0,0] neg_lo:[1,1] neg_hi:[0,1]
	s_nop 0
	v_pk_fma_f32 v[24:25], v[24:25], v[10:11], v[30:31] op_sel_hi:[1,0,1]
	v_pk_add_f32 v[30:31], v[18:19], v[26:27]
	v_pk_add_f32 v[18:19], v[18:19], v[26:27] neg_lo:[0,1] neg_hi:[0,1]
	s_nop 0
	v_xor_b32_e32 v27, 0x80000000, v18
	v_mov_b32_e32 v26, v19
	v_pk_add_f32 v[18:19], v[96:97], v[34:35]
	v_pk_add_f32 v[34:35], v[96:97], v[34:35] neg_lo:[0,1] neg_hi:[0,1]
	s_nop 0
	v_pk_mul_f32 v[46:47], v[34:35], v[10:11] op_sel:[1,0] op_sel_hi:[0,0] neg_lo:[1,1] neg_hi:[0,1]
	s_nop 0
	v_pk_fma_f32 v[34:35], v[34:35], v[10:11], v[46:47] op_sel_hi:[1,0,1] neg_lo:[0,1,0] neg_hi:[0,1,0]
	v_pk_add_f32 v[46:47], v[38:39], v[30:31]
	v_pk_add_f32 v[38:39], v[38:39], v[30:31] neg_lo:[0,1] neg_hi:[0,1]
	v_pk_add_f32 v[30:31], v[22:23], v[18:19]
	v_pk_add_f32 v[18:19], v[22:23], v[18:19] neg_lo:[0,1] neg_hi:[0,1]
	v_pk_add_f32 v[96:97], v[46:47], v[30:31]
	v_xor_b32_e32 v23, 0x80000000, v18
	v_mov_b32_e32 v22, v19
	v_pk_add_f32 v[18:19], v[104:105], v[26:27]
	v_pk_add_f32 v[104:105], v[104:105], v[26:27] neg_lo:[0,1] neg_hi:[0,1]
	v_pk_add_f32 v[26:27], v[24:25], v[34:35]
	v_pk_add_f32 v[24:25], v[24:25], v[34:35] neg_lo:[0,1] neg_hi:[0,1]
	v_pk_add_f32 v[30:31], v[46:47], v[30:31] neg_lo:[0,1] neg_hi:[0,1]
	v_xor_b32_e32 v35, 0x80000000, v24
	v_mov_b32_e32 v34, v25
	v_pk_add_f32 v[24:25], v[50:51], v[100:101]
	v_pk_add_f32 v[100:101], v[50:51], v[100:101] neg_lo:[0,1] neg_hi:[0,1]
	v_pk_add_f32 v[50:51], v[78:79], v[102:103] neg_lo:[0,1] neg_hi:[0,1]
	v_pk_add_f32 v[46:47], v[38:39], v[22:23]
	v_pk_add_f32 v[22:23], v[38:39], v[22:23] neg_lo:[0,1] neg_hi:[0,1]
	v_pk_add_f32 v[106:107], v[18:19], v[26:27]
	v_pk_add_f32 v[26:27], v[18:19], v[26:27] neg_lo:[0,1] neg_hi:[0,1]
	v_pk_add_f32 v[38:39], v[104:105], v[34:35]
	v_pk_add_f32 v[18:19], v[104:105], v[34:35] neg_lo:[0,1] neg_hi:[0,1]
	v_pk_add_f32 v[34:35], v[78:79], v[102:103]
	v_pk_mul_f32 v[78:79], v[10:11], v[50:51] op_sel:[0,1] op_sel_hi:[0,0] neg_lo:[1,1] neg_hi:[1,0]
	v_pk_fma_f32 v[78:79], v[10:11], v[50:51], v[78:79] op_sel_hi:[0,1,1]
	v_pk_add_f32 v[50:51], v[20:21], v[28:29]
	v_pk_add_f32 v[20:21], v[20:21], v[28:29] neg_lo:[0,1] neg_hi:[0,1]
	s_nop 0
	v_xor_b32_e32 v29, 0x80000000, v20
	v_mov_b32_e32 v28, v21
	v_pk_add_f32 v[20:21], v[98:99], v[42:43]
	v_pk_add_f32 v[42:43], v[98:99], v[42:43] neg_lo:[0,1] neg_hi:[0,1]
	s_nop 0
	v_pk_mul_f32 v[98:99], v[10:11], v[42:43] op_sel:[0,1] op_sel_hi:[0,0] neg_lo:[1,1] neg_hi:[1,0]
	v_pk_fma_f32 v[42:43], v[10:11], v[42:43], v[98:99] op_sel_hi:[0,1,1] neg_lo:[1,0,0] neg_hi:[1,0,0]
	v_pk_add_f32 v[98:99], v[24:25], v[50:51]
	v_pk_add_f32 v[24:25], v[24:25], v[50:51] neg_lo:[0,1] neg_hi:[0,1]
	v_pk_add_f32 v[50:51], v[34:35], v[20:21]
	v_pk_add_f32 v[20:21], v[34:35], v[20:21] neg_lo:[0,1] neg_hi:[0,1]
	v_pk_add_f32 v[104:105], v[98:99], v[50:51]
	v_xor_b32_e32 v103, 0x80000000, v20
	v_mov_b32_e32 v102, v21
	v_pk_add_f32 v[34:35], v[98:99], v[50:51] neg_lo:[0,1] neg_hi:[0,1]
	v_pk_add_f32 v[20:21], v[100:101], v[28:29]
	v_pk_add_f32 v[98:99], v[100:101], v[28:29] neg_lo:[0,1] neg_hi:[0,1]
	v_pk_add_f32 v[28:29], v[78:79], v[42:43]
	v_pk_add_f32 v[42:43], v[78:79], v[42:43] neg_lo:[0,1] neg_hi:[0,1]
	v_pk_add_f32 v[100:101], v[20:21], v[28:29]
	v_xor_b32_e32 v79, 0x80000000, v42
	v_mov_b32_e32 v78, v43
	v_pk_add_f32 v[28:29], v[20:21], v[28:29] neg_lo:[0,1] neg_hi:[0,1]
	v_pk_add_f32 v[42:43], v[98:99], v[78:79]
	v_pk_add_f32 v[20:21], v[98:99], v[78:79] neg_lo:[0,1] neg_hi:[0,1]
	v_pk_add_f32 v[78:79], v[40:41], v[94:95]
	v_pk_add_f32 v[94:95], v[40:41], v[94:95] neg_lo:[0,1] neg_hi:[0,1]
	v_pk_add_f32 v[40:41], v[44:45], v[80:81]
	v_pk_add_f32 v[44:45], v[44:45], v[80:81] neg_lo:[0,1] neg_hi:[0,1]
	v_pk_add_f32 v[50:51], v[24:25], v[102:103]
	v_pk_mul_f32 v[80:81], v[36:37], v[44:45] op_sel:[0,1] op_sel_hi:[0,0] neg_lo:[1,1] neg_hi:[1,0]
	v_pk_fma_f32 v[44:45], v[32:33], v[44:45], v[80:81] op_sel_hi:[0,1,1]
	v_pk_add_f32 v[80:81], v[48:49], v[82:83]
	v_pk_add_f32 v[48:49], v[48:49], v[82:83] neg_lo:[0,1] neg_hi:[0,1]
	v_pk_add_f32 v[24:25], v[24:25], v[102:103] neg_lo:[0,1] neg_hi:[0,1]
	v_pk_mul_f32 v[82:83], v[10:11], v[48:49] op_sel:[0,1] op_sel_hi:[0,0] neg_lo:[1,1] neg_hi:[1,0]
	v_pk_fma_f32 v[82:83], v[10:11], v[48:49], v[82:83] op_sel_hi:[0,1,1]
	v_pk_add_f32 v[48:49], v[52:53], v[84:85]
	v_pk_add_f32 v[52:53], v[52:53], v[84:85] neg_lo:[0,1] neg_hi:[0,1]
	s_nop 0
	v_pk_mul_f32 v[84:85], v[32:33], v[52:53] op_sel:[0,1] op_sel_hi:[0,0] neg_lo:[1,1] neg_hi:[1,0]
	v_pk_fma_f32 v[52:53], v[36:37], v[52:53], v[84:85] op_sel_hi:[0,1,1]
	v_pk_add_f32 v[84:85], v[54:55], v[86:87]
	v_pk_add_f32 v[54:55], v[54:55], v[86:87] neg_lo:[0,1] neg_hi:[0,1]
	s_nop 0
	v_xor_b32_e32 v87, 0x80000000, v54
	v_mov_b32_e32 v86, v55
	v_pk_add_f32 v[54:55], v[56:57], v[88:89]
	v_pk_add_f32 v[56:57], v[56:57], v[88:89] neg_lo:[0,1] neg_hi:[0,1]
	s_nop 0
	v_pk_mul_f32 v[88:89], v[32:33], v[56:57] op_sel:[0,1] op_sel_hi:[0,0] neg_lo:[1,1] neg_hi:[1,0]
	v_pk_fma_f32 v[56:57], v[36:37], v[56:57], v[88:89] op_sel_hi:[0,1,1] neg_lo:[1,0,0] neg_hi:[1,0,0]
	v_pk_add_f32 v[88:89], v[58:59], v[90:91]
	v_pk_add_f32 v[58:59], v[58:59], v[90:91] neg_lo:[0,1] neg_hi:[0,1]
	s_nop 0
	v_pk_mul_f32 v[90:91], v[10:11], v[58:59] op_sel:[0,1] op_sel_hi:[0,0] neg_lo:[1,1] neg_hi:[1,0]
	v_pk_fma_f32 v[58:59], v[10:11], v[58:59], v[90:91] op_sel_hi:[0,1,1] neg_lo:[1,0,0] neg_hi:[1,0,0]
	v_pk_add_f32 v[90:91], v[60:61], v[92:93]
	v_pk_add_f32 v[60:61], v[60:61], v[92:93] neg_lo:[0,1] neg_hi:[0,1]
	s_nop 0
	v_pk_mul_f32 v[36:37], v[36:37], v[60:61] op_sel:[0,1] op_sel_hi:[0,0] neg_lo:[1,1] neg_hi:[1,0]
	v_pk_fma_f32 v[36:37], v[32:33], v[60:61], v[36:37] op_sel_hi:[0,1,1] neg_lo:[1,0,0] neg_hi:[1,0,0]
	v_pk_add_f32 v[32:33], v[78:79], v[84:85]
	v_pk_add_f32 v[60:61], v[78:79], v[84:85] neg_lo:[0,1] neg_hi:[0,1]
	v_pk_add_f32 v[78:79], v[54:55], v[40:41]
	v_pk_add_f32 v[40:41], v[40:41], v[54:55] neg_lo:[0,1] neg_hi:[0,1]
	s_nop 0
	v_pk_mul_f32 v[54:55], v[10:11], v[40:41] op_sel:[0,1] op_sel_hi:[0,0] neg_lo:[1,1] neg_hi:[1,0]
	v_pk_fma_f32 v[54:55], v[10:11], v[40:41], v[54:55] op_sel_hi:[0,1,1]
	v_pk_add_f32 v[40:41], v[80:81], v[88:89]
	v_pk_add_f32 v[80:81], v[80:81], v[88:89] neg_lo:[0,1] neg_hi:[0,1]
	s_nop 0
	v_xor_b32_e32 v85, 0x80000000, v80
	v_mov_b32_e32 v84, v81
	v_pk_add_f32 v[80:81], v[48:49], v[90:91]
	v_pk_add_f32 v[48:49], v[48:49], v[90:91] neg_lo:[0,1] neg_hi:[0,1]
	v_pk_add_f32 v[90:91], v[78:79], v[80:81]
	v_pk_mul_f32 v[88:89], v[10:11], v[48:49] op_sel:[0,1] op_sel_hi:[0,0] neg_lo:[1,1] neg_hi:[1,0]
	v_pk_fma_f32 v[48:49], v[10:11], v[48:49], v[88:89] op_sel_hi:[0,1,1] neg_lo:[1,0,0] neg_hi:[1,0,0]
	v_pk_add_f32 v[88:89], v[32:33], v[40:41]
	v_pk_add_f32 v[32:33], v[32:33], v[40:41] neg_lo:[0,1] neg_hi:[0,1]
	v_pk_add_f32 v[40:41], v[78:79], v[80:81] neg_lo:[0,1] neg_hi:[0,1]
	v_pk_add_f32 v[80:81], v[88:89], v[90:91] neg_lo:[0,1] neg_hi:[0,1]
	v_pk_add_f32 v[92:93], v[32:33], v[40:41] op_sel:[0,1] op_sel_hi:[1,0] neg_hi:[0,1]
	v_pk_add_f32 v[40:41], v[32:33], v[40:41] op_sel:[0,1] op_sel_hi:[1,0] neg_lo:[0,1]
	v_pk_add_f32 v[78:79], v[54:55], v[48:49]
	v_pk_add_f32 v[48:49], v[54:55], v[48:49] neg_lo:[0,1] neg_hi:[0,1]
	v_pk_add_f32 v[32:33], v[60:61], v[84:85]
	v_pk_add_f32 v[60:61], v[60:61], v[84:85] neg_lo:[0,1] neg_hi:[0,1]
	v_xor_b32_e32 v55, 0x80000000, v48
	v_mov_b32_e32 v54, v49
	v_pk_add_f32 v[84:85], v[32:33], v[78:79]
	v_pk_add_f32 v[48:49], v[32:33], v[78:79] neg_lo:[0,1] neg_hi:[0,1]
	v_pk_add_f32 v[78:79], v[60:61], v[54:55]
	v_pk_add_f32 v[32:33], v[60:61], v[54:55] neg_lo:[0,1] neg_hi:[0,1]
	v_pk_add_f32 v[54:55], v[94:95], v[86:87]
	v_pk_add_f32 v[60:61], v[94:95], v[86:87] neg_lo:[0,1] neg_hi:[0,1]
	v_pk_add_f32 v[86:87], v[56:57], v[44:45]
	v_pk_add_f32 v[44:45], v[44:45], v[56:57] neg_lo:[0,1] neg_hi:[0,1]
	v_pk_add_f32 v[88:89], v[88:89], v[90:91]
	v_pk_mul_f32 v[56:57], v[10:11], v[44:45] op_sel:[0,1] op_sel_hi:[0,0] neg_lo:[1,1] neg_hi:[1,0]
	v_pk_fma_f32 v[56:57], v[10:11], v[44:45], v[56:57] op_sel_hi:[0,1,1]
	v_pk_add_f32 v[44:45], v[82:83], v[58:59]
	v_pk_add_f32 v[58:59], v[82:83], v[58:59] neg_lo:[0,1] neg_hi:[0,1]
	s_nop 0
	v_xor_b32_e32 v83, 0x80000000, v58
	v_mov_b32_e32 v82, v59
	v_pk_add_f32 v[58:59], v[52:53], v[36:37]
	v_pk_add_f32 v[36:37], v[52:53], v[36:37] neg_lo:[0,1] neg_hi:[0,1]
	s_nop 0
	v_pk_mul_f32 v[52:53], v[10:11], v[36:37] op_sel:[0,1] op_sel_hi:[0,0] neg_lo:[1,1] neg_hi:[1,0]
	v_pk_fma_f32 v[36:37], v[10:11], v[36:37], v[52:53] op_sel_hi:[0,1,1] neg_lo:[1,0,0] neg_hi:[1,0,0]
	v_pk_add_f32 v[52:53], v[54:55], v[44:45]
	v_pk_add_f32 v[44:45], v[54:55], v[44:45] neg_lo:[0,1] neg_hi:[0,1]
	v_pk_add_f32 v[54:55], v[86:87], v[58:59]
	v_pk_add_f32 v[58:59], v[86:87], v[58:59] neg_lo:[0,1] neg_hi:[0,1]
	s_nop 0
	v_xor_b32_e32 v87, 0x80000000, v58
	v_mov_b32_e32 v86, v59
	v_pk_add_f32 v[58:59], v[52:53], v[54:55]
	v_pk_add_f32 v[54:55], v[52:53], v[54:55] neg_lo:[0,1] neg_hi:[0,1]
	v_pk_add_f32 v[52:53], v[60:61], v[82:83]
	v_pk_add_f32 v[60:61], v[60:61], v[82:83] neg_lo:[0,1] neg_hi:[0,1]
	v_pk_add_f32 v[82:83], v[56:57], v[36:37]
	v_pk_add_f32 v[36:37], v[56:57], v[36:37] neg_lo:[0,1] neg_hi:[0,1]
	v_pk_add_f32 v[94:95], v[44:45], v[86:87]
	v_pk_add_f32 v[44:45], v[44:45], v[86:87] neg_lo:[0,1] neg_hi:[0,1]
	v_pk_add_f32 v[86:87], v[52:53], v[82:83]
	v_pk_add_f32 v[52:53], v[52:53], v[82:83] neg_lo:[0,1] neg_hi:[0,1]
	v_pk_add_f32 v[82:83], v[60:61], v[36:37] op_sel:[0,1] op_sel_hi:[1,0] neg_hi:[0,1]
	v_pk_add_f32 v[36:37], v[60:61], v[36:37] op_sel:[0,1] op_sel_hi:[1,0] neg_lo:[0,1]
	v_pk_fma_f32 v[60:61], v[14:15], s[90:91], v[14:15] op_sel:[1,0,0] op_sel_hi:[0,1,1]
	v_pk_mul_f32 v[56:57], v[96:97], s[14:15] op_sel:[1,0] neg_lo:[1,0]
	v_pk_mul_f32 v[90:91], v[60:61], v[88:89] op_sel:[1,1] op_sel_hi:[0,1] neg_lo:[0,1]
	v_pk_fma_f32 v[56:57], v[96:97], s[94:95], v[56:57] op_sel_hi:[0,1,1]
	v_pk_fma_f32 v[88:89], v[60:61], v[88:89], v[90:91] op_sel_hi:[1,0,1]
	ds_write2_b64 v76, v[56:57], v[88:89] offset1:16
	v_pk_mul_f32 v[56:57], v[14:15], v[60:61] op_sel:[1,1] op_sel_hi:[0,1] neg_lo:[0,1]
	v_pk_fma_f32 v[56:57], v[14:15], v[60:61], v[56:57] op_sel_hi:[1,0,1]
	s_nop 0
	v_pk_mul_f32 v[60:61], v[56:57], v[104:105] op_sel:[1,1] op_sel_hi:[0,1] neg_lo:[0,1]
	v_pk_mul_f32 v[76:77], v[14:15], v[56:57] op_sel:[1,1] op_sel_hi:[0,1] neg_lo:[0,1]
	v_pk_fma_f32 v[60:61], v[56:57], v[104:105], v[60:61] op_sel_hi:[1,0,1]
	v_pk_fma_f32 v[56:57], v[14:15], v[56:57], v[76:77] op_sel_hi:[1,0,1]
	s_nop 0
	v_pk_mul_f32 v[76:77], v[56:57], v[58:59] op_sel:[1,1] op_sel_hi:[0,1] neg_lo:[0,1]
	v_pk_fma_f32 v[58:59], v[56:57], v[58:59], v[76:77] op_sel_hi:[1,0,1]
	ds_write2_b64 v75, v[60:61], v[58:59] offset0:32 offset1:48
	v_pk_mul_f32 v[58:59], v[14:15], v[56:57] op_sel:[1,1] op_sel_hi:[0,1] neg_lo:[0,1]
	v_pk_fma_f32 v[56:57], v[14:15], v[56:57], v[58:59] op_sel_hi:[1,0,1]
	s_nop 0
	v_pk_mul_f32 v[58:59], v[56:57], v[106:107] op_sel:[1,1] op_sel_hi:[0,1] neg_lo:[0,1]
	v_pk_mul_f32 v[60:61], v[14:15], v[56:57] op_sel:[1,1] op_sel_hi:[0,1] neg_lo:[0,1]
	v_pk_fma_f32 v[58:59], v[56:57], v[106:107], v[58:59] op_sel_hi:[1,0,1]
	v_pk_fma_f32 v[56:57], v[14:15], v[56:57], v[60:61] op_sel_hi:[1,0,1]
	s_nop 0
	v_pk_mul_f32 v[60:61], v[56:57], v[84:85] op_sel:[1,1] op_sel_hi:[0,1] neg_lo:[0,1]
	v_pk_fma_f32 v[60:61], v[56:57], v[84:85], v[60:61] op_sel_hi:[1,0,1]
	ds_write2_b64 v74, v[58:59], v[60:61] offset0:64 offset1:80
	v_pk_mul_f32 v[58:59], v[14:15], v[56:57] op_sel:[1,1] op_sel_hi:[0,1] neg_lo:[0,1]
	v_pk_fma_f32 v[56:57], v[14:15], v[56:57], v[58:59] op_sel_hi:[1,0,1]
	s_nop 0
	v_pk_mul_f32 v[58:59], v[56:57], v[100:101] op_sel:[1,1] op_sel_hi:[0,1] neg_lo:[0,1]
	v_pk_mul_f32 v[60:61], v[14:15], v[56:57] op_sel:[1,1] op_sel_hi:[0,1] neg_lo:[0,1]
	v_pk_fma_f32 v[58:59], v[56:57], v[100:101], v[58:59] op_sel_hi:[1,0,1]
	v_pk_fma_f32 v[56:57], v[14:15], v[56:57], v[60:61] op_sel_hi:[1,0,1]
	s_nop 0
	v_pk_mul_f32 v[60:61], v[56:57], v[86:87] op_sel:[1,1] op_sel_hi:[0,1] neg_lo:[0,1]
	v_pk_fma_f32 v[60:61], v[56:57], v[86:87], v[60:61] op_sel_hi:[1,0,1]
	ds_write2_b64 v73, v[58:59], v[60:61] offset0:96 offset1:112
	v_pk_mul_f32 v[58:59], v[14:15], v[56:57] op_sel:[1,1] op_sel_hi:[0,1] neg_lo:[0,1]
	v_pk_fma_f32 v[56:57], v[14:15], v[56:57], v[58:59] op_sel_hi:[1,0,1]
	s_nop 0
	v_pk_mul_f32 v[58:59], v[56:57], v[46:47] op_sel:[1,1] op_sel_hi:[0,1] neg_lo:[0,1]
	v_pk_fma_f32 v[46:47], v[56:57], v[46:47], v[58:59] op_sel_hi:[1,0,1]
	v_pk_mul_f32 v[58:59], v[14:15], v[56:57] op_sel:[1,1] op_sel_hi:[0,1] neg_lo:[0,1]
	v_pk_fma_f32 v[56:57], v[14:15], v[56:57], v[58:59] op_sel_hi:[1,0,1]
	s_nop 0
	v_pk_mul_f32 v[58:59], v[56:57], v[92:93] op_sel:[1,1] op_sel_hi:[0,1] neg_lo:[0,1]
	v_pk_fma_f32 v[58:59], v[56:57], v[92:93], v[58:59] op_sel_hi:[1,0,1]
	ds_write2_b64 v72, v[46:47], v[58:59] offset0:128 offset1:144
	v_pk_mul_f32 v[46:47], v[14:15], v[56:57] op_sel:[1,1] op_sel_hi:[0,1] neg_lo:[0,1]
	v_pk_fma_f32 v[46:47], v[14:15], v[56:57], v[46:47] op_sel_hi:[1,0,1]
	s_nop 0
	v_pk_mul_f32 v[56:57], v[46:47], v[50:51] op_sel:[1,1] op_sel_hi:[0,1] neg_lo:[0,1]
	v_pk_fma_f32 v[50:51], v[46:47], v[50:51], v[56:57] op_sel_hi:[1,0,1]
	v_pk_mul_f32 v[56:57], v[14:15], v[46:47] op_sel:[1,1] op_sel_hi:[0,1] neg_lo:[0,1]
	v_pk_fma_f32 v[46:47], v[14:15], v[46:47], v[56:57] op_sel_hi:[1,0,1]
	s_nop 0
	v_pk_mul_f32 v[56:57], v[46:47], v[94:95] op_sel:[1,1] op_sel_hi:[0,1] neg_lo:[0,1]
	v_pk_fma_f32 v[56:57], v[46:47], v[94:95], v[56:57] op_sel_hi:[1,0,1]
	ds_write2_b64 v71, v[50:51], v[56:57] offset0:160 offset1:176
	v_pk_mul_f32 v[50:51], v[14:15], v[46:47] op_sel:[1,1] op_sel_hi:[0,1] neg_lo:[0,1]
	v_pk_fma_f32 v[46:47], v[14:15], v[46:47], v[50:51] op_sel_hi:[1,0,1]
	s_nop 0
	v_pk_mul_f32 v[50:51], v[38:39], v[46:47] op_sel:[1,1] op_sel_hi:[1,0] neg_lo:[1,0]
	s_nop 0
	v_pk_fma_f32 v[38:39], v[38:39], v[46:47], v[50:51] op_sel_hi:[0,1,1]
	v_pk_mul_f32 v[50:51], v[14:15], v[46:47] op_sel:[1,1] op_sel_hi:[0,1] neg_lo:[0,1]
	v_pk_fma_f32 v[46:47], v[14:15], v[46:47], v[50:51] op_sel_hi:[1,0,1]
	s_nop 0
	v_pk_mul_f32 v[50:51], v[46:47], v[78:79] op_sel:[1,1] op_sel_hi:[0,1] neg_lo:[0,1]
	v_pk_fma_f32 v[50:51], v[46:47], v[78:79], v[50:51] op_sel_hi:[1,0,1]
	ds_write2_b64 v70, v[38:39], v[50:51] offset0:192 offset1:208
	v_pk_mul_f32 v[38:39], v[14:15], v[46:47] op_sel:[1,1] op_sel_hi:[0,1] neg_lo:[0,1]
	v_pk_fma_f32 v[38:39], v[14:15], v[46:47], v[38:39] op_sel_hi:[1,0,1]
	s_nop 0
	v_pk_mul_f32 v[46:47], v[42:43], v[38:39] op_sel:[1,1] op_sel_hi:[1,0] neg_lo:[1,0]
	s_nop 0
	v_pk_fma_f32 v[42:43], v[42:43], v[38:39], v[46:47] op_sel_hi:[0,1,1]
	v_pk_mul_f32 v[46:47], v[14:15], v[38:39] op_sel:[1,1] op_sel_hi:[0,1] neg_lo:[0,1]
	v_pk_fma_f32 v[38:39], v[14:15], v[38:39], v[46:47] op_sel_hi:[1,0,1]
	s_nop 0
	v_pk_mul_f32 v[46:47], v[38:39], v[82:83] op_sel:[1,1] op_sel_hi:[0,1] neg_lo:[0,1]
	v_pk_fma_f32 v[46:47], v[38:39], v[82:83], v[46:47] op_sel_hi:[1,0,1]
	ds_write2_b64 v69, v[42:43], v[46:47] offset0:224 offset1:240
	v_pk_mul_f32 v[42:43], v[14:15], v[38:39] op_sel:[1,1] op_sel_hi:[0,1] neg_lo:[0,1]
	v_pk_fma_f32 v[38:39], v[14:15], v[38:39], v[42:43] op_sel_hi:[1,0,1]
	s_nop 0
	v_pk_mul_f32 v[42:43], v[30:31], v[38:39] op_sel:[1,1] op_sel_hi:[1,0] neg_lo:[1,0]
	s_nop 0
	v_pk_fma_f32 v[30:31], v[30:31], v[38:39], v[42:43] op_sel_hi:[0,1,1]
	v_pk_mul_f32 v[42:43], v[14:15], v[38:39] op_sel:[1,1] op_sel_hi:[0,1] neg_lo:[0,1]
	v_pk_fma_f32 v[38:39], v[14:15], v[38:39], v[42:43] op_sel_hi:[1,0,1]
	s_nop 0
	v_pk_mul_f32 v[42:43], v[80:81], v[38:39] op_sel:[1,1] op_sel_hi:[1,0] neg_lo:[1,0]
	s_nop 0
	v_pk_fma_f32 v[42:43], v[80:81], v[38:39], v[42:43] op_sel_hi:[0,1,1]
	ds_write2_b64 v68, v[30:31], v[42:43] offset1:16
	v_pk_mul_f32 v[30:31], v[14:15], v[38:39] op_sel:[1,1] op_sel_hi:[0,1] neg_lo:[0,1]
	v_pk_fma_f32 v[30:31], v[14:15], v[38:39], v[30:31] op_sel_hi:[1,0,1]
	s_nop 0
	v_pk_mul_f32 v[38:39], v[34:35], v[30:31] op_sel:[1,1] op_sel_hi:[1,0] neg_lo:[1,0]
	s_nop 0
	v_pk_fma_f32 v[34:35], v[34:35], v[30:31], v[38:39] op_sel_hi:[0,1,1]
	v_pk_mul_f32 v[38:39], v[14:15], v[30:31] op_sel:[1,1] op_sel_hi:[0,1] neg_lo:[0,1]
	v_pk_fma_f32 v[30:31], v[14:15], v[30:31], v[38:39] op_sel_hi:[1,0,1]
	s_nop 0
	v_pk_mul_f32 v[38:39], v[54:55], v[30:31] op_sel:[1,1] op_sel_hi:[1,0] neg_lo:[1,0]
	s_nop 0
	v_pk_fma_f32 v[38:39], v[54:55], v[30:31], v[38:39] op_sel_hi:[0,1,1]
	ds_write2_b64 v67, v[34:35], v[38:39] offset0:32 offset1:48
	v_pk_mul_f32 v[34:35], v[14:15], v[30:31] op_sel:[1,1] op_sel_hi:[0,1] neg_lo:[0,1]
	v_pk_fma_f32 v[30:31], v[14:15], v[30:31], v[34:35] op_sel_hi:[1,0,1]
	s_nop 0
	v_pk_mul_f32 v[34:35], v[26:27], v[30:31] op_sel:[1,1] op_sel_hi:[1,0] neg_lo:[1,0]
	s_nop 0
	v_pk_fma_f32 v[26:27], v[26:27], v[30:31], v[34:35] op_sel_hi:[0,1,1]
	v_pk_mul_f32 v[34:35], v[14:15], v[30:31] op_sel:[1,1] op_sel_hi:[0,1] neg_lo:[0,1]
	v_pk_fma_f32 v[30:31], v[14:15], v[30:31], v[34:35] op_sel_hi:[1,0,1]
	s_nop 0
	v_pk_mul_f32 v[34:35], v[48:49], v[30:31] op_sel:[1,1] op_sel_hi:[1,0] neg_lo:[1,0]
	s_nop 0
	v_pk_fma_f32 v[34:35], v[48:49], v[30:31], v[34:35] op_sel_hi:[0,1,1]
	ds_write2_b64 v66, v[26:27], v[34:35] offset0:64 offset1:80
	v_pk_mul_f32 v[26:27], v[14:15], v[30:31] op_sel:[1,1] op_sel_hi:[0,1] neg_lo:[0,1]
	v_pk_fma_f32 v[26:27], v[14:15], v[30:31], v[26:27] op_sel_hi:[1,0,1]
	s_nop 0
	v_pk_mul_f32 v[30:31], v[28:29], v[26:27] op_sel:[1,1] op_sel_hi:[1,0] neg_lo:[1,0]
	s_nop 0
	v_pk_fma_f32 v[28:29], v[28:29], v[26:27], v[30:31] op_sel_hi:[0,1,1]
	v_pk_mul_f32 v[30:31], v[14:15], v[26:27] op_sel:[1,1] op_sel_hi:[0,1] neg_lo:[0,1]
	v_pk_fma_f32 v[26:27], v[14:15], v[26:27], v[30:31] op_sel_hi:[1,0,1]
	s_nop 0
	v_pk_mul_f32 v[30:31], v[52:53], v[26:27] op_sel:[1,1] op_sel_hi:[1,0] neg_lo:[1,0]
	s_nop 0
	v_pk_fma_f32 v[30:31], v[52:53], v[26:27], v[30:31] op_sel_hi:[0,1,1]
	ds_write2_b64 v65, v[28:29], v[30:31] offset0:96 offset1:112
	v_pk_mul_f32 v[28:29], v[14:15], v[26:27] op_sel:[1,1] op_sel_hi:[0,1] neg_lo:[0,1]
	v_pk_fma_f32 v[26:27], v[14:15], v[26:27], v[28:29] op_sel_hi:[1,0,1]
	s_nop 0
	v_pk_mul_f32 v[28:29], v[22:23], v[26:27] op_sel:[1,1] op_sel_hi:[1,0] neg_lo:[1,0]
	s_nop 0
	v_pk_fma_f32 v[22:23], v[22:23], v[26:27], v[28:29] op_sel_hi:[0,1,1]
	v_pk_mul_f32 v[28:29], v[14:15], v[26:27] op_sel:[1,1] op_sel_hi:[0,1] neg_lo:[0,1]
	v_pk_fma_f32 v[26:27], v[14:15], v[26:27], v[28:29] op_sel_hi:[1,0,1]
	s_nop 0
	v_pk_mul_f32 v[28:29], v[40:41], v[26:27] op_sel:[1,1] op_sel_hi:[1,0] neg_lo:[1,0]
	s_nop 0
	v_pk_fma_f32 v[28:29], v[40:41], v[26:27], v[28:29] op_sel_hi:[0,1,1]
	ds_write2_b64 v64, v[22:23], v[28:29] offset0:128 offset1:144
	v_pk_mul_f32 v[22:23], v[14:15], v[26:27] op_sel:[1,1] op_sel_hi:[0,1] neg_lo:[0,1]
	v_pk_fma_f32 v[22:23], v[14:15], v[26:27], v[22:23] op_sel_hi:[1,0,1]
	s_nop 0
	v_pk_mul_f32 v[26:27], v[24:25], v[22:23] op_sel:[1,1] op_sel_hi:[1,0] neg_lo:[1,0]
	s_nop 0
	v_pk_fma_f32 v[24:25], v[24:25], v[22:23], v[26:27] op_sel_hi:[0,1,1]
	v_pk_mul_f32 v[26:27], v[14:15], v[22:23] op_sel:[1,1] op_sel_hi:[0,1] neg_lo:[0,1]
	v_pk_fma_f32 v[22:23], v[14:15], v[22:23], v[26:27] op_sel_hi:[1,0,1]
	s_nop 0
	v_pk_mul_f32 v[26:27], v[44:45], v[22:23] op_sel:[1,1] op_sel_hi:[1,0] neg_lo:[1,0]
	s_nop 0
	v_pk_fma_f32 v[26:27], v[44:45], v[22:23], v[26:27] op_sel_hi:[0,1,1]
	ds_write2_b64 v63, v[24:25], v[26:27] offset0:160 offset1:176
	v_pk_mul_f32 v[24:25], v[14:15], v[22:23] op_sel:[1,1] op_sel_hi:[0,1] neg_lo:[0,1]
	v_pk_fma_f32 v[22:23], v[14:15], v[22:23], v[24:25] op_sel_hi:[1,0,1]
	s_nop 0
	v_pk_mul_f32 v[24:25], v[18:19], v[22:23] op_sel:[1,1] op_sel_hi:[1,0] neg_lo:[1,0]
	s_nop 0
	v_pk_fma_f32 v[18:19], v[18:19], v[22:23], v[24:25] op_sel_hi:[0,1,1]
	v_pk_mul_f32 v[24:25], v[14:15], v[22:23] op_sel:[1,1] op_sel_hi:[0,1] neg_lo:[0,1]
	v_pk_fma_f32 v[22:23], v[14:15], v[22:23], v[24:25] op_sel_hi:[1,0,1]
	s_nop 0
	v_pk_mul_f32 v[24:25], v[32:33], v[22:23] op_sel:[1,1] op_sel_hi:[1,0] neg_lo:[1,0]
	s_nop 0
	v_pk_fma_f32 v[24:25], v[32:33], v[22:23], v[24:25] op_sel_hi:[0,1,1]
	ds_write2_b64 v62, v[18:19], v[24:25] offset0:192 offset1:208
	v_pk_mul_f32 v[18:19], v[14:15], v[22:23] op_sel:[1,1] op_sel_hi:[0,1] neg_lo:[0,1]
	v_pk_fma_f32 v[18:19], v[14:15], v[22:23], v[18:19] op_sel_hi:[1,0,1]
	s_nop 0
	v_pk_mul_f32 v[22:23], v[20:21], v[18:19] op_sel:[1,1] op_sel_hi:[1,0] neg_lo:[1,0]
	s_nop 0
	v_pk_fma_f32 v[20:21], v[20:21], v[18:19], v[22:23] op_sel_hi:[0,1,1]
	v_pk_mul_f32 v[22:23], v[14:15], v[18:19] op_sel:[1,1] op_sel_hi:[0,1] neg_lo:[0,1]
	v_pk_fma_f32 v[14:15], v[14:15], v[18:19], v[22:23] op_sel_hi:[1,0,1]
	s_nop 0
	v_pk_mul_f32 v[18:19], v[36:37], v[14:15] op_sel:[1,1] op_sel_hi:[1,0] neg_lo:[1,0]
	s_nop 0
	v_pk_fma_f32 v[14:15], v[36:37], v[14:15], v[18:19] op_sel_hi:[0,1,1]
	ds_write2_b64 v13, v[20:21], v[14:15] offset0:224 offset1:240
	v_mov_b32_e32 v14, v182
	v_mov_b32_e32 v10, v176
	v_mov_b32_e32 v13, v175
	s_waitcnt lgkmcnt(0)
	s_barrier
	v_mov_b32_e32 v50, v167
	v_xor_b32_e32 v18, 1, v13
	v_lshlrev_b32_e32 v10, 3, v10
	v_lshlrev_b32_e32 v18, 3, v18
	v_add3_u32 v20, 0, v18, v10
	v_xor_b32_e32 v18, 2, v13
	v_lshlrev_b32_e32 v18, 3, v18
	v_xor_b32_e32 v26, 5, v13
	v_add3_u32 v22, 0, v18, v10
	v_xor_b32_e32 v18, 3, v13
	v_lshlrev_b32_e32 v26, 3, v26
	v_lshlrev_b32_e32 v15, 3, v13
	v_lshlrev_b32_e32 v18, 3, v18
	v_add3_u32 v28, 0, v26, v10
	v_xor_b32_e32 v26, 6, v13
	v_add3_u32 v15, 0, v15, v10
	v_add3_u32 v24, 0, v18, v10
	v_lshlrev_b32_e32 v26, 3, v26
	v_xor_b32_e32 v34, 9, v13
	ds_read_b64 v[18:19], v15
	ds_read_b64 v[20:21], v20
	ds_read_b64 v[22:23], v22
	ds_read_b64 v[24:25], v24
	v_xor_b32_e32 v15, 4, v13
	v_add3_u32 v30, 0, v26, v10
	v_xor_b32_e32 v26, 7, v13
	v_lshlrev_b32_e32 v34, 3, v34
	v_lshlrev_b32_e32 v15, 3, v15
	v_lshlrev_b32_e32 v26, 3, v26
	v_add3_u32 v36, 0, v34, v10
	v_xor_b32_e32 v34, 10, v13
	v_add3_u32 v15, 0, v15, v10
	v_add3_u32 v32, 0, v26, v10
	v_lshlrev_b32_e32 v34, 3, v34
	ds_read_b64 v[26:27], v15
	ds_read_b64 v[28:29], v28
	ds_read_b64 v[30:31], v30
	ds_read_b64 v[32:33], v32
	v_xor_b32_e32 v15, 8, v13
	v_add3_u32 v38, 0, v34, v10
	v_xor_b32_e32 v34, 11, v13
	v_lshlrev_b32_e32 v15, 3, v15
	v_lshlrev_b32_e32 v34, 3, v34
	v_xor_b32_e32 v42, 13, v13
	v_add3_u32 v15, 0, v15, v10
	v_add3_u32 v40, 0, v34, v10
	v_lshlrev_b32_e32 v42, 3, v42
	ds_read_b64 v[34:35], v15
	ds_read_b64 v[36:37], v36
	ds_read_b64 v[38:39], v38
	ds_read_b64 v[40:41], v40
	v_xor_b32_e32 v15, 12, v13
	v_add3_u32 v44, 0, v42, v10
	v_xor_b32_e32 v42, 14, v13
	v_xor_b32_e32 v13, 15, v13
	v_lshlrev_b32_e32 v15, 3, v15
	v_lshlrev_b32_e32 v42, 3, v42
	v_lshlrev_b32_e32 v13, 3, v13
	v_add3_u32 v15, 0, v15, v10
	v_add3_u32 v46, 0, v42, v10
	v_add3_u32 v10, 0, v13, v10
	ds_read_b64 v[42:43], v15
	ds_read_b64 v[44:45], v44
	ds_read_b64 v[46:47], v46
	ds_read_b64 v[48:49], v10
	s_waitcnt lgkmcnt(7)
	v_pk_add_f32 v[54:55], v[18:19], v[34:35]
	v_mov_b32_e32 v10, v165
	v_pk_add_f32 v[18:19], v[18:19], v[34:35] neg_lo:[0,1] neg_hi:[0,1]
	s_waitcnt lgkmcnt(6)
	v_pk_add_f32 v[34:35], v[20:21], v[36:37]
	v_pk_add_f32 v[20:21], v[20:21], v[36:37] neg_lo:[0,1] neg_hi:[0,1]
	v_mov_b32_e32 v52, v169
	v_ashrrev_i32_e32 v15, 31, v14
	v_pk_mul_f32 v[36:37], v[20:21], v[52:53] op_sel:[1,0] op_sel_hi:[0,0] neg_lo:[1,1] neg_hi:[0,1]
	v_pk_fma_f32 v[20:21], v[20:21], v[10:11], v[36:37] op_sel_hi:[1,0,1]
	s_waitcnt lgkmcnt(5)
	v_pk_add_f32 v[36:37], v[22:23], v[38:39]
	v_pk_add_f32 v[22:23], v[22:23], v[38:39] neg_lo:[0,1] neg_hi:[0,1]
	s_movk_i32 s0, 0x1000
	v_pk_mul_f32 v[38:39], v[22:23], v[50:51] op_sel:[1,0] op_sel_hi:[0,0] neg_lo:[1,1] neg_hi:[0,1]
	v_pk_fma_f32 v[22:23], v[22:23], v[50:51], v[38:39] op_sel_hi:[1,0,1]
	s_waitcnt lgkmcnt(4)
	v_pk_add_f32 v[38:39], v[24:25], v[40:41]
	v_pk_add_f32 v[24:25], v[24:25], v[40:41] neg_lo:[0,1] neg_hi:[0,1]
	v_mov_b32_e32 v72, v164
	v_pk_mul_f32 v[40:41], v[24:25], v[52:53] op_sel_hi:[1,0]
	s_nop 0
	v_pk_fma_f32 v[24:25], v[24:25], v[10:11], v[40:41] op_sel:[1,0,0] op_sel_hi:[0,0,1] neg_lo:[1,1,0] neg_hi:[0,1,0]
	s_waitcnt lgkmcnt(3)
	v_pk_add_f32 v[40:41], v[26:27], v[42:43]
	v_pk_add_f32 v[26:27], v[26:27], v[42:43] neg_lo:[0,1] neg_hi:[0,1]
	v_mov_b32_e32 v13, v175
	v_xor_b32_e32 v43, 0x80000000, v26
	v_mov_b32_e32 v42, v27
	s_waitcnt lgkmcnt(2)
	v_pk_add_f32 v[26:27], v[28:29], v[44:45]
	v_pk_add_f32 v[28:29], v[28:29], v[44:45] neg_lo:[0,1] neg_hi:[0,1]
	v_mov_b32_e32 v74, v166
	v_pk_mul_f32 v[44:45], v[28:29], v[52:53] op_sel_hi:[1,0] neg_lo:[0,1] neg_hi:[0,1]
	s_nop 0
	v_pk_fma_f32 v[28:29], v[28:29], v[10:11], v[44:45] op_sel:[1,0,0] op_sel_hi:[0,0,1] neg_lo:[1,1,0] neg_hi:[0,1,0]
	s_waitcnt lgkmcnt(1)
	v_pk_add_f32 v[44:45], v[30:31], v[46:47]
	v_pk_add_f32 v[30:31], v[30:31], v[46:47] neg_lo:[0,1] neg_hi:[0,1]
	v_mov_b32_e32 v76, v168
	v_pk_mul_f32 v[46:47], v[30:31], v[50:51] op_sel:[1,0] op_sel_hi:[0,0] neg_lo:[1,1] neg_hi:[0,1]
	v_mov_b32_e32 v78, v170
	v_pk_fma_f32 v[30:31], v[30:31], v[50:51], v[46:47] op_sel_hi:[1,0,1] neg_lo:[0,1,0] neg_hi:[0,1,0]
	s_waitcnt lgkmcnt(0)
	v_pk_add_f32 v[46:47], v[32:33], v[48:49]
	v_pk_add_f32 v[32:33], v[32:33], v[48:49] neg_lo:[0,1] neg_hi:[0,1]
	v_mov_b32_e32 v83, v11
	v_pk_mul_f32 v[48:49], v[32:33], v[52:53] op_sel:[1,0] op_sel_hi:[0,0] neg_lo:[1,1] neg_hi:[0,1]
	v_pk_add_f32 v[52:53], v[34:35], v[26:27]
	v_pk_add_f32 v[26:27], v[34:35], v[26:27] neg_lo:[0,1] neg_hi:[0,1]
	v_pk_fma_f32 v[32:33], v[32:33], v[10:11], v[48:49] op_sel_hi:[1,0,1] neg_lo:[0,1,0] neg_hi:[0,1,0]
	v_pk_mul_f32 v[34:35], v[26:27], v[50:51] op_sel:[1,0] op_sel_hi:[0,0] neg_lo:[1,1] neg_hi:[0,1]
	v_pk_add_f32 v[48:49], v[54:55], v[40:41]
	v_pk_fma_f32 v[26:27], v[26:27], v[50:51], v[34:35] op_sel_hi:[1,0,1]
	v_pk_add_f32 v[34:35], v[36:37], v[44:45]
	v_pk_add_f32 v[36:37], v[36:37], v[44:45] neg_lo:[0,1] neg_hi:[0,1]
	v_pk_add_f32 v[40:41], v[54:55], v[40:41] neg_lo:[0,1] neg_hi:[0,1]
	v_xor_b32_e32 v45, 0x80000000, v36
	v_mov_b32_e32 v44, v37
	v_pk_add_f32 v[36:37], v[38:39], v[46:47]
	v_pk_add_f32 v[38:39], v[38:39], v[46:47] neg_lo:[0,1] neg_hi:[0,1]
	v_mov_b32_e32 v10, v177
	v_pk_mul_f32 v[46:47], v[38:39], v[50:51] op_sel:[1,0] op_sel_hi:[0,0] neg_lo:[1,1] neg_hi:[0,1]
	s_mov_b32 s7, 0xa000
	v_pk_fma_f32 v[38:39], v[38:39], v[50:51], v[46:47] op_sel_hi:[1,0,1] neg_lo:[0,1,0] neg_hi:[0,1,0]
	v_pk_add_f32 v[46:47], v[48:49], v[34:35]
	v_pk_add_f32 v[34:35], v[48:49], v[34:35] neg_lo:[0,1] neg_hi:[0,1]
	v_pk_add_f32 v[48:49], v[52:53], v[36:37]
	v_pk_add_f32 v[36:37], v[52:53], v[36:37] neg_lo:[0,1] neg_hi:[0,1]
	s_mov_b32 s6, 0xc000
	v_xor_b32_e32 v53, 0x80000000, v36
	v_mov_b32_e32 v52, v37
	v_pk_add_f32 v[36:37], v[46:47], v[48:49]
	v_pk_add_f32 v[46:47], v[46:47], v[48:49] neg_lo:[0,1] neg_hi:[0,1]
	v_pk_add_f32 v[48:49], v[34:35], v[52:53]
	v_pk_add_f32 v[34:35], v[34:35], v[52:53] neg_lo:[0,1] neg_hi:[0,1]
	v_pk_add_f32 v[52:53], v[40:41], v[44:45]
	v_pk_add_f32 v[40:41], v[40:41], v[44:45] neg_lo:[0,1] neg_hi:[0,1]
	v_pk_add_f32 v[44:45], v[26:27], v[38:39]
	v_pk_add_f32 v[26:27], v[26:27], v[38:39] neg_lo:[0,1] neg_hi:[0,1]
	s_mov_b32 s1, 0xe000
	v_xor_b32_e32 v39, 0x80000000, v26
	v_mov_b32_e32 v38, v27
	v_pk_add_f32 v[26:27], v[52:53], v[44:45]
	v_pk_add_f32 v[44:45], v[52:53], v[44:45] neg_lo:[0,1] neg_hi:[0,1]
	v_pk_add_f32 v[52:53], v[40:41], v[38:39]
	v_pk_add_f32 v[38:39], v[40:41], v[38:39] neg_lo:[0,1] neg_hi:[0,1]
	v_pk_add_f32 v[40:41], v[18:19], v[42:43]
	v_pk_add_f32 v[18:19], v[18:19], v[42:43] neg_lo:[0,1] neg_hi:[0,1]
	v_pk_add_f32 v[42:43], v[20:21], v[28:29]
	v_pk_add_f32 v[20:21], v[20:21], v[28:29] neg_lo:[0,1] neg_hi:[0,1]
	s_mov_b32 s8, 0x8000
	v_pk_mul_f32 v[28:29], v[50:51], v[20:21] op_sel:[0,1] op_sel_hi:[0,0] neg_lo:[1,1] neg_hi:[1,0]
	v_pk_fma_f32 v[20:21], v[50:51], v[20:21], v[28:29] op_sel_hi:[0,1,1]
	v_pk_add_f32 v[28:29], v[22:23], v[30:31]
	v_pk_add_f32 v[22:23], v[22:23], v[30:31] neg_lo:[0,1] neg_hi:[0,1]
	s_mov_b32 s9, 0x9000
	v_xor_b32_e32 v31, 0x80000000, v22
	v_mov_b32_e32 v30, v23
	v_pk_add_f32 v[22:23], v[24:25], v[32:33]
	v_pk_add_f32 v[24:25], v[24:25], v[32:33] neg_lo:[0,1] neg_hi:[0,1]
	s_mov_b32 s5, 0xb000
	v_pk_mul_f32 v[32:33], v[50:51], v[24:25] op_sel:[0,1] op_sel_hi:[0,0] neg_lo:[1,1] neg_hi:[1,0]
	v_pk_fma_f32 v[24:25], v[50:51], v[24:25], v[32:33] op_sel_hi:[0,1,1] neg_lo:[1,0,0] neg_hi:[1,0,0]
	v_pk_add_f32 v[32:33], v[40:41], v[28:29]
	v_pk_add_f32 v[28:29], v[40:41], v[28:29] neg_lo:[0,1] neg_hi:[0,1]
	v_pk_add_f32 v[40:41], v[42:43], v[22:23]
	v_pk_add_f32 v[22:23], v[42:43], v[22:23] neg_lo:[0,1] neg_hi:[0,1]
	v_mov_b32_e32 v50, v167
	v_xor_b32_e32 v43, 0x80000000, v22
	v_mov_b32_e32 v42, v23
	v_pk_add_f32 v[22:23], v[32:33], v[40:41]
	v_pk_add_f32 v[32:33], v[32:33], v[40:41] neg_lo:[0,1] neg_hi:[0,1]
	v_pk_add_f32 v[40:41], v[28:29], v[42:43]
	v_pk_add_f32 v[28:29], v[28:29], v[42:43] neg_lo:[0,1] neg_hi:[0,1]
	v_pk_add_f32 v[42:43], v[18:19], v[30:31]
	v_pk_add_f32 v[18:19], v[18:19], v[30:31] neg_lo:[0,1] neg_hi:[0,1]
	v_pk_add_f32 v[30:31], v[20:21], v[24:25]
	v_pk_add_f32 v[20:21], v[20:21], v[24:25] neg_lo:[0,1] neg_hi:[0,1]
	s_mov_b32 s4, 0xd000
	v_xor_b32_e32 v25, 0x80000000, v20
	v_mov_b32_e32 v24, v21
	v_pk_add_f32 v[20:21], v[42:43], v[30:31]
	v_pk_add_f32 v[30:31], v[42:43], v[30:31] neg_lo:[0,1] neg_hi:[0,1]
	v_pk_add_f32 v[42:43], v[18:19], v[24:25]
	v_pk_add_f32 v[18:19], v[18:19], v[24:25] neg_lo:[0,1] neg_hi:[0,1]
	v_lshl_add_u64 v[24:25], v[14:15], 3, s[46:47]
	global_store_dwordx2 v[24:25], v[36:37], off
	v_add_u32_e32 v24, 0x200, v14
	v_ashrrev_i32_e32 v25, 31, v24
	v_lshl_add_u64 v[24:25], v[24:25], 3, s[46:47]
	global_store_dwordx2 v[24:25], v[22:23], off
	v_add_u32_e32 v22, 0x400, v14
	v_ashrrev_i32_e32 v23, 31, v22
	v_lshl_add_u64 v[22:23], v[22:23], 3, s[46:47]
	global_store_dwordx2 v[22:23], v[26:27], off
	v_add_u32_e32 v22, 0x600, v14
	v_ashrrev_i32_e32 v23, 31, v22
	v_lshl_add_u64 v[22:23], v[22:23], 3, s[46:47]
	global_store_dwordx2 v[22:23], v[20:21], off
	v_add_u32_e32 v20, 0x800, v14
	v_ashrrev_i32_e32 v21, 31, v20
	v_lshl_add_u64 v[20:21], v[20:21], 3, s[46:47]
	global_store_dwordx2 v[20:21], v[48:49], off
	v_add_u32_e32 v20, 0xa00, v14
	v_ashrrev_i32_e32 v21, 31, v20
	v_lshl_add_u64 v[20:21], v[20:21], 3, s[46:47]
	global_store_dwordx2 v[20:21], v[40:41], off
	v_add_u32_e32 v20, 0xc00, v14
	v_ashrrev_i32_e32 v21, 31, v20
	v_lshl_add_u64 v[20:21], v[20:21], 3, s[46:47]
	global_store_dwordx2 v[20:21], v[52:53], off
	v_add_u32_e32 v20, 0xe00, v14
	v_ashrrev_i32_e32 v21, 31, v20
	v_lshl_add_u64 v[20:21], v[20:21], 3, s[46:47]
	global_store_dwordx2 v[20:21], v[42:43], off
	v_add_u32_e32 v20, 0x1000, v14
	v_ashrrev_i32_e32 v21, 31, v20
	v_lshl_add_u64 v[20:21], v[20:21], 3, s[46:47]
	global_store_dwordx2 v[20:21], v[46:47], off
	v_add_u32_e32 v20, 0x1200, v14
	v_ashrrev_i32_e32 v21, 31, v20
	v_lshl_add_u64 v[20:21], v[20:21], 3, s[46:47]
	global_store_dwordx2 v[20:21], v[32:33], off
	v_add_u32_e32 v20, 0x1400, v14
	v_ashrrev_i32_e32 v21, 31, v20
	v_lshl_add_u64 v[20:21], v[20:21], 3, s[46:47]
	global_store_dwordx2 v[20:21], v[44:45], off
	v_add_u32_e32 v20, 0x1600, v14
	v_ashrrev_i32_e32 v21, 31, v20
	v_lshl_add_u64 v[20:21], v[20:21], 3, s[46:47]
	global_store_dwordx2 v[20:21], v[30:31], off
	v_add_u32_e32 v20, 0x1800, v14
	v_ashrrev_i32_e32 v21, 31, v20
	v_lshl_add_u64 v[20:21], v[20:21], 3, s[46:47]
	global_store_dwordx2 v[20:21], v[34:35], off
	v_add_u32_e32 v20, 0x1a00, v14
	v_ashrrev_i32_e32 v21, 31, v20
	v_lshl_add_u64 v[20:21], v[20:21], 3, s[46:47]
	global_store_dwordx2 v[20:21], v[28:29], off
	v_add_u32_e32 v20, 0x1c00, v14
	v_ashrrev_i32_e32 v21, 31, v20
	v_lshl_add_u64 v[20:21], v[20:21], 3, s[46:47]
	global_store_dwordx2 v[20:21], v[38:39], off
	v_add_u32_e32 v20, 0x1e00, v14
	v_ashrrev_i32_e32 v21, 31, v20
	v_lshl_add_u64 v[20:21], v[20:21], 3, s[46:47]
	global_store_dwordx2 v[20:21], v[18:19], off
	v_mov_b32_e32 v52, v169
	v_xor_b32_e32 v18, 1, v13
	v_lshlrev_b32_e32 v10, 3, v10
	v_lshlrev_b32_e32 v18, 3, v18
	v_add3_u32 v20, 0, v18, v10
	v_xor_b32_e32 v18, 2, v13
	v_lshlrev_b32_e32 v18, 3, v18
	v_xor_b32_e32 v26, 5, v13
	v_add3_u32 v22, 0, v18, v10
	v_xor_b32_e32 v18, 3, v13
	v_lshlrev_b32_e32 v26, 3, v26
	v_lshlrev_b32_e32 v15, 3, v13
	v_lshlrev_b32_e32 v18, 3, v18
	v_add3_u32 v28, 0, v26, v10
	v_xor_b32_e32 v26, 6, v13
	v_add3_u32 v15, 0, v15, v10
	v_add3_u32 v24, 0, v18, v10
	v_lshlrev_b32_e32 v26, 3, v26
	v_xor_b32_e32 v34, 9, v13
	ds_read_b64 v[18:19], v15
	ds_read_b64 v[20:21], v20
	ds_read_b64 v[22:23], v22
	ds_read_b64 v[24:25], v24
	v_xor_b32_e32 v15, 4, v13
	v_add3_u32 v30, 0, v26, v10
	v_xor_b32_e32 v26, 7, v13
	v_lshlrev_b32_e32 v34, 3, v34
	v_lshlrev_b32_e32 v15, 3, v15
	v_lshlrev_b32_e32 v26, 3, v26
	v_add3_u32 v36, 0, v34, v10
	v_xor_b32_e32 v34, 10, v13
	v_add3_u32 v15, 0, v15, v10
	v_add3_u32 v32, 0, v26, v10
	v_lshlrev_b32_e32 v34, 3, v34
	ds_read_b64 v[26:27], v15
	ds_read_b64 v[28:29], v28
	ds_read_b64 v[30:31], v30
	ds_read_b64 v[32:33], v32
	v_xor_b32_e32 v15, 8, v13
	v_add3_u32 v38, 0, v34, v10
	v_xor_b32_e32 v34, 11, v13
	v_lshlrev_b32_e32 v15, 3, v15
	v_lshlrev_b32_e32 v34, 3, v34
	v_xor_b32_e32 v42, 13, v13
	v_add3_u32 v15, 0, v15, v10
	v_add3_u32 v40, 0, v34, v10
	v_lshlrev_b32_e32 v42, 3, v42
	ds_read_b64 v[34:35], v15
	ds_read_b64 v[36:37], v36
	ds_read_b64 v[38:39], v38
	ds_read_b64 v[40:41], v40
	v_xor_b32_e32 v15, 12, v13
	v_add3_u32 v44, 0, v42, v10
	v_xor_b32_e32 v42, 14, v13
	v_xor_b32_e32 v13, 15, v13
	v_lshlrev_b32_e32 v15, 3, v15
	v_lshlrev_b32_e32 v42, 3, v42
	v_lshlrev_b32_e32 v13, 3, v13
	v_add3_u32 v15, 0, v15, v10
	v_add3_u32 v46, 0, v42, v10
	v_add3_u32 v10, 0, v13, v10
	ds_read_b64 v[42:43], v15
	ds_read_b64 v[44:45], v44
	ds_read_b64 v[46:47], v46
	ds_read_b64 v[48:49], v10
	s_waitcnt lgkmcnt(7)
	v_pk_add_f32 v[54:55], v[18:19], v[34:35]
	v_mov_b32_e32 v10, v165
	v_pk_add_f32 v[18:19], v[18:19], v[34:35] neg_lo:[0,1] neg_hi:[0,1]
	s_waitcnt lgkmcnt(6)
	v_pk_add_f32 v[34:35], v[20:21], v[36:37]
	v_pk_add_f32 v[20:21], v[20:21], v[36:37] neg_lo:[0,1] neg_hi:[0,1]
	s_nop 0
	v_pk_mul_f32 v[36:37], v[20:21], v[52:53] op_sel:[1,0] op_sel_hi:[0,0] neg_lo:[1,1] neg_hi:[0,1]
	v_pk_fma_f32 v[20:21], v[20:21], v[10:11], v[36:37] op_sel_hi:[1,0,1]
	s_waitcnt lgkmcnt(5)
	v_pk_add_f32 v[36:37], v[22:23], v[38:39]
	v_pk_add_f32 v[22:23], v[22:23], v[38:39] neg_lo:[0,1] neg_hi:[0,1]
	s_nop 0
	v_pk_mul_f32 v[38:39], v[22:23], v[50:51] op_sel:[1,0] op_sel_hi:[0,0] neg_lo:[1,1] neg_hi:[0,1]
	v_pk_fma_f32 v[22:23], v[22:23], v[50:51], v[38:39] op_sel_hi:[1,0,1]
	s_waitcnt lgkmcnt(4)
	v_pk_add_f32 v[38:39], v[24:25], v[40:41]
	v_pk_add_f32 v[24:25], v[24:25], v[40:41] neg_lo:[0,1] neg_hi:[0,1]
	s_nop 0
	v_pk_mul_f32 v[40:41], v[24:25], v[52:53] op_sel_hi:[1,0]
	s_nop 0
	v_pk_fma_f32 v[24:25], v[24:25], v[10:11], v[40:41] op_sel:[1,0,0] op_sel_hi:[0,0,1] neg_lo:[1,1,0] neg_hi:[0,1,0]
	s_waitcnt lgkmcnt(3)
	v_pk_add_f32 v[40:41], v[26:27], v[42:43]
	v_pk_add_f32 v[26:27], v[26:27], v[42:43] neg_lo:[0,1] neg_hi:[0,1]
	s_nop 0
	v_xor_b32_e32 v43, 0x80000000, v26
	v_mov_b32_e32 v42, v27
	s_waitcnt lgkmcnt(2)
	v_pk_add_f32 v[26:27], v[28:29], v[44:45]
	v_pk_add_f32 v[28:29], v[28:29], v[44:45] neg_lo:[0,1] neg_hi:[0,1]
	s_nop 0
	v_pk_mul_f32 v[44:45], v[28:29], v[52:53] op_sel_hi:[1,0] neg_lo:[0,1] neg_hi:[0,1]
	s_nop 0
	v_pk_fma_f32 v[28:29], v[28:29], v[10:11], v[44:45] op_sel:[1,0,0] op_sel_hi:[0,0,1] neg_lo:[1,1,0] neg_hi:[0,1,0]
	s_waitcnt lgkmcnt(1)
	v_pk_add_f32 v[44:45], v[30:31], v[46:47]
	v_pk_add_f32 v[30:31], v[30:31], v[46:47] neg_lo:[0,1] neg_hi:[0,1]
	s_nop 0
	v_pk_mul_f32 v[46:47], v[30:31], v[50:51] op_sel:[1,0] op_sel_hi:[0,0] neg_lo:[1,1] neg_hi:[0,1]
	s_nop 0
	v_pk_fma_f32 v[30:31], v[30:31], v[50:51], v[46:47] op_sel_hi:[1,0,1] neg_lo:[0,1,0] neg_hi:[0,1,0]
	s_waitcnt lgkmcnt(0)
	v_pk_add_f32 v[46:47], v[32:33], v[48:49]
	v_pk_add_f32 v[32:33], v[32:33], v[48:49] neg_lo:[0,1] neg_hi:[0,1]
	s_nop 0
	v_pk_mul_f32 v[48:49], v[32:33], v[52:53] op_sel:[1,0] op_sel_hi:[0,0] neg_lo:[1,1] neg_hi:[0,1]
	v_pk_add_f32 v[52:53], v[34:35], v[26:27]
	v_pk_add_f32 v[26:27], v[34:35], v[26:27] neg_lo:[0,1] neg_hi:[0,1]
	v_pk_fma_f32 v[32:33], v[32:33], v[10:11], v[48:49] op_sel_hi:[1,0,1] neg_lo:[0,1,0] neg_hi:[0,1,0]
	v_pk_mul_f32 v[34:35], v[26:27], v[50:51] op_sel:[1,0] op_sel_hi:[0,0] neg_lo:[1,1] neg_hi:[0,1]
	v_pk_add_f32 v[48:49], v[54:55], v[40:41]
	v_pk_fma_f32 v[26:27], v[26:27], v[50:51], v[34:35] op_sel_hi:[1,0,1]
	v_pk_add_f32 v[34:35], v[36:37], v[44:45]
	v_pk_add_f32 v[36:37], v[36:37], v[44:45] neg_lo:[0,1] neg_hi:[0,1]
	v_pk_add_f32 v[40:41], v[54:55], v[40:41] neg_lo:[0,1] neg_hi:[0,1]
	v_xor_b32_e32 v45, 0x80000000, v36
	v_mov_b32_e32 v44, v37
	v_pk_add_f32 v[36:37], v[38:39], v[46:47]
	v_pk_add_f32 v[38:39], v[38:39], v[46:47] neg_lo:[0,1] neg_hi:[0,1]
	v_pk_mul_f32 v[46:47], v[38:39], v[50:51] op_sel:[1,0] op_sel_hi:[0,0] neg_lo:[1,1] neg_hi:[0,1]
	s_nop 0
	v_pk_fma_f32 v[38:39], v[38:39], v[50:51], v[46:47] op_sel_hi:[1,0,1] neg_lo:[0,1,0] neg_hi:[0,1,0]
	v_pk_add_f32 v[46:47], v[48:49], v[34:35]
	v_pk_add_f32 v[34:35], v[48:49], v[34:35] neg_lo:[0,1] neg_hi:[0,1]
	v_pk_add_f32 v[48:49], v[52:53], v[36:37]
	v_pk_add_f32 v[36:37], v[52:53], v[36:37] neg_lo:[0,1] neg_hi:[0,1]
	s_nop 0
	v_xor_b32_e32 v53, 0x80000000, v36
	v_mov_b32_e32 v52, v37
	v_pk_add_f32 v[36:37], v[46:47], v[48:49]
	v_pk_add_f32 v[46:47], v[46:47], v[48:49] neg_lo:[0,1] neg_hi:[0,1]
	v_pk_add_f32 v[48:49], v[34:35], v[52:53]
	v_pk_add_f32 v[34:35], v[34:35], v[52:53] neg_lo:[0,1] neg_hi:[0,1]
	v_pk_add_f32 v[52:53], v[40:41], v[44:45]
	v_pk_add_f32 v[40:41], v[40:41], v[44:45] neg_lo:[0,1] neg_hi:[0,1]
	v_pk_add_f32 v[44:45], v[26:27], v[38:39]
	v_pk_add_f32 v[26:27], v[26:27], v[38:39] neg_lo:[0,1] neg_hi:[0,1]
	s_nop 0
	v_xor_b32_e32 v39, 0x80000000, v26
	v_mov_b32_e32 v38, v27
	v_pk_add_f32 v[26:27], v[52:53], v[44:45]
	v_pk_add_f32 v[44:45], v[52:53], v[44:45] neg_lo:[0,1] neg_hi:[0,1]
	v_pk_add_f32 v[52:53], v[40:41], v[38:39]
	v_pk_add_f32 v[38:39], v[40:41], v[38:39] neg_lo:[0,1] neg_hi:[0,1]
	v_pk_add_f32 v[40:41], v[18:19], v[42:43]
	v_pk_add_f32 v[18:19], v[18:19], v[42:43] neg_lo:[0,1] neg_hi:[0,1]
	v_pk_add_f32 v[42:43], v[20:21], v[28:29]
	v_pk_add_f32 v[20:21], v[20:21], v[28:29] neg_lo:[0,1] neg_hi:[0,1]
	s_nop 0
	v_pk_mul_f32 v[28:29], v[50:51], v[20:21] op_sel:[0,1] op_sel_hi:[0,0] neg_lo:[1,1] neg_hi:[1,0]
	v_pk_fma_f32 v[20:21], v[50:51], v[20:21], v[28:29] op_sel_hi:[0,1,1]
	v_pk_add_f32 v[28:29], v[22:23], v[30:31]
	v_pk_add_f32 v[22:23], v[22:23], v[30:31] neg_lo:[0,1] neg_hi:[0,1]
	s_nop 0
	v_xor_b32_e32 v31, 0x80000000, v22
	v_mov_b32_e32 v30, v23
	v_pk_add_f32 v[22:23], v[24:25], v[32:33]
	v_pk_add_f32 v[24:25], v[24:25], v[32:33] neg_lo:[0,1] neg_hi:[0,1]
	s_nop 0
	v_pk_mul_f32 v[32:33], v[50:51], v[24:25] op_sel:[0,1] op_sel_hi:[0,0] neg_lo:[1,1] neg_hi:[1,0]
	v_pk_fma_f32 v[24:25], v[50:51], v[24:25], v[32:33] op_sel_hi:[0,1,1] neg_lo:[1,0,0] neg_hi:[1,0,0]
	v_pk_add_f32 v[32:33], v[40:41], v[28:29]
	v_pk_add_f32 v[28:29], v[40:41], v[28:29] neg_lo:[0,1] neg_hi:[0,1]
	v_pk_add_f32 v[40:41], v[42:43], v[22:23]
	v_pk_add_f32 v[22:23], v[42:43], v[22:23] neg_lo:[0,1] neg_hi:[0,1]
	s_nop 0
	v_xor_b32_e32 v43, 0x80000000, v22
	v_mov_b32_e32 v42, v23
	v_pk_add_f32 v[22:23], v[32:33], v[40:41]
	v_pk_add_f32 v[32:33], v[32:33], v[40:41] neg_lo:[0,1] neg_hi:[0,1]
	v_pk_add_f32 v[40:41], v[28:29], v[42:43]
	v_pk_add_f32 v[28:29], v[28:29], v[42:43] neg_lo:[0,1] neg_hi:[0,1]
	v_pk_add_f32 v[42:43], v[18:19], v[30:31]
	v_pk_add_f32 v[18:19], v[18:19], v[30:31] neg_lo:[0,1] neg_hi:[0,1]
	v_pk_add_f32 v[30:31], v[20:21], v[24:25]
	v_pk_add_f32 v[20:21], v[20:21], v[24:25] neg_lo:[0,1] neg_hi:[0,1]
	s_nop 0
	v_xor_b32_e32 v25, 0x80000000, v20
	v_mov_b32_e32 v24, v21
	v_pk_add_f32 v[20:21], v[42:43], v[30:31]
	v_pk_add_f32 v[30:31], v[42:43], v[30:31] neg_lo:[0,1] neg_hi:[0,1]
	v_pk_add_f32 v[42:43], v[18:19], v[24:25]
	v_pk_add_f32 v[18:19], v[18:19], v[24:25] neg_lo:[0,1] neg_hi:[0,1]
	v_add_u32_e32 v24, 0x2000, v14
	v_ashrrev_i32_e32 v25, 31, v24
	v_lshl_add_u64 v[24:25], v[24:25], 3, s[46:47]
	global_store_dwordx2 v[24:25], v[36:37], off
	v_add_u32_e32 v24, 0x2200, v14
	v_ashrrev_i32_e32 v25, 31, v24
	v_lshl_add_u64 v[24:25], v[24:25], 3, s[46:47]
	global_store_dwordx2 v[24:25], v[22:23], off
	v_add_u32_e32 v22, 0x2400, v14
	v_ashrrev_i32_e32 v23, 31, v22
	v_lshl_add_u64 v[22:23], v[22:23], 3, s[46:47]
	global_store_dwordx2 v[22:23], v[26:27], off
	v_add_u32_e32 v22, 0x2600, v14
	v_ashrrev_i32_e32 v23, 31, v22
	v_lshl_add_u64 v[22:23], v[22:23], 3, s[46:47]
	global_store_dwordx2 v[22:23], v[20:21], off
	v_add_u32_e32 v20, 0x2800, v14
	v_ashrrev_i32_e32 v21, 31, v20
	v_lshl_add_u64 v[20:21], v[20:21], 3, s[46:47]
	global_store_dwordx2 v[20:21], v[48:49], off
	v_add_u32_e32 v20, 0x2a00, v14
	v_ashrrev_i32_e32 v21, 31, v20
	v_lshl_add_u64 v[20:21], v[20:21], 3, s[46:47]
	global_store_dwordx2 v[20:21], v[40:41], off
	v_add_u32_e32 v20, 0x2c00, v14
	v_ashrrev_i32_e32 v21, 31, v20
	v_lshl_add_u64 v[20:21], v[20:21], 3, s[46:47]
	global_store_dwordx2 v[20:21], v[52:53], off
	v_add_u32_e32 v20, 0x2e00, v14
	v_ashrrev_i32_e32 v21, 31, v20
	v_lshl_add_u64 v[20:21], v[20:21], 3, s[46:47]
	global_store_dwordx2 v[20:21], v[42:43], off
	v_add_u32_e32 v20, 0x3000, v14
	v_ashrrev_i32_e32 v21, 31, v20
	v_lshl_add_u64 v[20:21], v[20:21], 3, s[46:47]
	global_store_dwordx2 v[20:21], v[46:47], off
	v_add_u32_e32 v20, 0x3200, v14
	v_ashrrev_i32_e32 v21, 31, v20
	v_lshl_add_u64 v[20:21], v[20:21], 3, s[46:47]
	global_store_dwordx2 v[20:21], v[32:33], off
	v_add_u32_e32 v20, 0x3400, v14
	v_ashrrev_i32_e32 v21, 31, v20
	v_lshl_add_u64 v[20:21], v[20:21], 3, s[46:47]
	global_store_dwordx2 v[20:21], v[44:45], off
	v_add_u32_e32 v20, 0x3600, v14
	v_ashrrev_i32_e32 v21, 31, v20
	v_lshl_add_u64 v[20:21], v[20:21], 3, s[46:47]
	global_store_dwordx2 v[20:21], v[30:31], off
	v_add_u32_e32 v20, 0x3800, v14
	v_ashrrev_i32_e32 v21, 31, v20
	v_lshl_add_u64 v[20:21], v[20:21], 3, s[46:47]
	global_store_dwordx2 v[20:21], v[34:35], off
	v_add_u32_e32 v20, 0x3a00, v14
	v_ashrrev_i32_e32 v21, 31, v20
	v_lshl_add_u64 v[20:21], v[20:21], 3, s[46:47]
	global_store_dwordx2 v[20:21], v[28:29], off
	v_add_u32_e32 v20, 0x3c00, v14
	v_add_u32_e32 v14, 0x3e00, v14
	v_ashrrev_i32_e32 v15, 31, v14
	v_ashrrev_i32_e32 v21, 31, v20
	v_lshl_add_u64 v[14:15], v[14:15], 3, s[46:47]
	v_lshl_add_u64 v[20:21], v[20:21], 3, s[46:47]
	global_store_dwordx2 v[14:15], v[18:19], off
	v_mov_b32_e32 v14, v182
	global_store_dwordx2 v[20:21], v[38:39], off
	s_barrier
	v_mov_b32_e32 v40, v169
	v_ashrrev_i32_e32 v15, 31, v14
	v_lshl_add_u64 v[18:19], v[14:15], 2, s[64:65]
	v_add_co_u32_e32 v28, vcc, s0, v18
	s_movk_i32 s0, 0x2000
	s_nop 0
	v_addc_co_u32_e32 v29, vcc, 0, v19, vcc
	v_add_co_u32_e32 v22, vcc, s0, v18
	s_movk_i32 s0, 0x6000
	s_nop 0
	v_addc_co_u32_e32 v23, vcc, 0, v19, vcc
	v_add_co_u32_e32 v30, vcc, s78, v18
	global_load_dword v20, v[18:19], off
	global_load_dword v21, v[18:19], off offset:2048
	v_addc_co_u32_e32 v31, vcc, 0, v19, vcc
	v_add_co_u32_e32 v32, vcc, s43, v18
	v_mov_b32_e32 v15, v173
	s_nop 0
	v_addc_co_u32_e32 v33, vcc, 0, v19, vcc
	v_add_co_u32_e32 v34, vcc, s0, v18
	s_mov_b32 s0, 0x8000
	s_nop 0
	v_addc_co_u32_e32 v35, vcc, 0, v19, vcc
	v_add_co_u32_e32 v36, vcc, s0, v18
	s_mov_b32 s0, 0xa000
	s_nop 0
	v_addc_co_u32_e32 v37, vcc, 0, v19, vcc
	v_add_co_u32_e32 v38, vcc, s0, v18
	global_load_dword v26, v[22:23], off offset:-4096
	global_load_dword v24, v[22:23], off
	global_load_dword v25, v[22:23], off offset:2048
	s_nop 0
	global_load_dword v22, v[32:33], off offset:-4096
	v_addc_co_u32_e32 v39, vcc, 0, v19, vcc
	global_load_dword v43, v[32:33], off offset:2048
	global_load_dword v46, v[34:35], off offset:-4096
	global_load_dword v48, v[36:37], off
	global_load_dword v49, v[36:37], off offset:2048
	global_load_dword v62, v[34:35], off
	global_load_dword v63, v[34:35], off offset:2048
	s_nop 0
	global_load_dword v34, v[38:39], off offset:-4096
	global_load_dword v64, v[36:37], off offset:-4096
	s_mov_b32 s0, 0x9000
	v_add_co_u32_e32 v36, vcc, s0, v18
	s_movk_i32 s0, 0x5000
	s_nop 0
	v_addc_co_u32_e32 v37, vcc, 0, v19, vcc
	global_load_dword v27, v[28:29], off offset:2048
	global_load_dword v35, v[36:37], off offset:2048
	v_add_co_u32_e32 v28, vcc, s0, v18
	s_mov_b32 s0, 0xb000
	s_nop 0
	v_addc_co_u32_e32 v29, vcc, 0, v19, vcc
	global_load_dword v66, v[38:39], off
	global_load_dword v67, v[38:39], off offset:2048
	v_add_co_u32_e32 v36, vcc, s0, v18
	s_mov_b32 s0, 0xc000
	s_nop 0
	v_addc_co_u32_e32 v37, vcc, 0, v19, vcc
	v_add_co_u32_e32 v38, vcc, s0, v18
	s_movk_i32 s0, 0x7000
	s_nop 0
	v_addc_co_u32_e32 v39, vcc, 0, v19, vcc
	global_load_dword v68, v[38:39], off offset:-4096
	global_load_dword v23, v[30:31], off offset:2048
	global_load_dword v69, v[36:37], off offset:2048
	v_add_co_u32_e32 v30, vcc, s0, v18
	s_mov_b32 s0, 0xe000
	s_nop 0
	v_addc_co_u32_e32 v31, vcc, 0, v19, vcc
	global_load_dword v47, v[28:29], off offset:2048
	global_load_dword v65, v[30:31], off offset:2048
	global_load_dword v42, v[32:33], off
	s_nop 0
	global_load_dword v30, v[38:39], off
	global_load_dword v31, v[38:39], off offset:2048
	v_add_co_u32_e32 v28, vcc, s0, v18
	s_mov_b32 s0, 0xd000
	s_nop 0
	v_addc_co_u32_e32 v29, vcc, 0, v19, vcc
	global_load_dword v32, v[28:29], off offset:-4096
	v_add_co_u32_e32 v36, vcc, s0, v18
	s_mov_b32 s0, 0xf000
	s_nop 0
	v_addc_co_u32_e32 v37, vcc, 0, v19, vcc
	global_load_dword v33, v[36:37], off offset:2048
	global_load_dword v38, v[28:29], off
	global_load_dword v39, v[28:29], off offset:2048
	v_add_co_u32_e32 v18, vcc, s0, v18
	v_mov_b32_e32 v36, v165
	s_nop 0
	v_addc_co_u32_e32 v19, vcc, 0, v19, vcc
	global_load_dword v70, v[18:19], off
	global_load_dword v71, v[18:19], off offset:2048
	v_mov_b32_e32 v28, v167
	v_mov_b32_e32 v45, v11
	s_waitcnt vmcnt(22)
	v_sub_f32_e32 v44, v21, v49
	v_mov_b32_e32 v13, v44
	v_pk_mul_f32 v[50:51], v[12:13], v[78:79] op_sel_hi:[1,0] neg_lo:[0,1] neg_hi:[0,1]
	v_sub_f32_e32 v10, v20, v48
	v_pk_fma_f32 v[44:45], v[44:45], v[72:73], v[50:51] op_sel_hi:[1,0,1]
	s_waitcnt vmcnt(19)
	v_sub_f32_e32 v50, v26, v34
	v_mov_b32_e32 v13, v50
	v_mov_b32_e32 v51, v11
	v_pk_mul_f32 v[52:53], v[12:13], v[40:41] op_sel_hi:[1,0] neg_lo:[0,1] neg_hi:[0,1]
	v_pk_add_f32 v[20:21], v[20:21], v[48:49]
	v_pk_fma_f32 v[50:51], v[50:51], v[36:37], v[52:53] op_sel_hi:[1,0,1]
	s_waitcnt vmcnt(16)
	v_sub_f32_e32 v52, v27, v35
	v_mov_b32_e32 v13, v52
	v_mov_b32_e32 v53, v11
	v_pk_mul_f32 v[54:55], v[12:13], v[76:77] op_sel_hi:[1,0] neg_lo:[0,1] neg_hi:[0,1]
	v_pk_add_f32 v[26:27], v[26:27], v[34:35]
	v_pk_fma_f32 v[54:55], v[52:53], v[74:75], v[54:55] op_sel_hi:[1,0,1]
	s_waitcnt vmcnt(15)
	v_sub_f32_e32 v52, v24, v66
	v_mov_b32_e32 v13, v52
	v_pk_mul_f32 v[56:57], v[12:13], v[28:29] op_sel_hi:[1,0] neg_lo:[0,1] neg_hi:[0,1]
	s_waitcnt vmcnt(6)
	v_sub_f32_e32 v82, v43, v31
	v_pk_fma_f32 v[56:57], v[52:53], v[28:29], v[56:57] op_sel_hi:[1,0,1]
	v_sub_f32_e32 v52, v25, v67
	v_pk_mul_f32 v[58:59], v[52:53], v[76:77] op_sel_hi:[1,0]
	v_mov_b32_e32 v13, v52
	v_sub_f32_e32 v52, v22, v68
	v_pk_fma_f32 v[60:61], v[12:13], v[74:75], v[58:59] op_sel_hi:[1,0,1] neg_lo:[0,1,0] neg_hi:[0,1,0]
	v_pk_mul_f32 v[58:59], v[52:53], v[40:41] op_sel_hi:[1,0]
	v_mov_b32_e32 v13, v52
	v_sub_f32_e32 v52, v23, v69
	v_pk_fma_f32 v[58:59], v[12:13], v[36:37], v[58:59] op_sel_hi:[1,0,1] neg_lo:[0,1,0] neg_hi:[0,1,0]
	v_pk_mul_f32 v[80:81], v[52:53], v[78:79] op_sel_hi:[1,0]
	v_mov_b32_e32 v13, v52
	v_pk_fma_f32 v[52:53], v[12:13], v[72:73], v[80:81] op_sel_hi:[1,0,1] neg_lo:[0,1,0] neg_hi:[0,1,0]
	v_sub_f32_e32 v13, v42, v30
	v_xor_b32_e32 v81, 0x80000000, v13
	v_pk_mul_f32 v[84:85], v[82:83], v[78:79] op_sel_hi:[1,0] neg_lo:[0,1] neg_hi:[0,1]
	v_mov_b32_e32 v13, v82
	v_pk_fma_f32 v[82:83], v[12:13], v[72:73], v[84:85] op_sel_hi:[1,0,1] neg_lo:[0,1,0] neg_hi:[0,1,0]
	s_waitcnt vmcnt(5)
	v_sub_f32_e32 v84, v46, v32
	v_mov_b32_e32 v85, v11
	v_pk_mul_f32 v[86:87], v[84:85], v[40:41] op_sel_hi:[1,0] neg_lo:[0,1] neg_hi:[0,1]
	v_mov_b32_e32 v13, v84
	v_pk_fma_f32 v[84:85], v[12:13], v[36:37], v[86:87] op_sel_hi:[1,0,1] neg_lo:[0,1,0] neg_hi:[0,1,0]
	s_waitcnt vmcnt(4)
	v_sub_f32_e32 v86, v47, v33
	v_mov_b32_e32 v87, v11
	v_pk_mul_f32 v[88:89], v[86:87], v[76:77] op_sel_hi:[1,0] neg_lo:[0,1] neg_hi:[0,1]
	v_mov_b32_e32 v13, v86
	v_pk_fma_f32 v[86:87], v[12:13], v[74:75], v[88:89] op_sel_hi:[1,0,1] neg_lo:[0,1,0] neg_hi:[0,1,0]
	s_waitcnt vmcnt(3)
	v_sub_f32_e32 v88, v62, v38
	v_mov_b32_e32 v13, v88
	v_mov_b32_e32 v89, v11
	v_pk_mul_f32 v[90:91], v[12:13], v[28:29] op_sel_hi:[1,0] neg_lo:[0,1] neg_hi:[0,1]
	v_pk_add_f32 v[30:31], v[42:43], v[30:31]
	v_pk_fma_f32 v[88:89], v[88:89], v[28:29], v[90:91] op_sel_hi:[1,0,1] neg_lo:[0,1,0] neg_hi:[0,1,0]
	s_waitcnt vmcnt(2)
	v_sub_f32_e32 v90, v63, v39
	v_mov_b32_e32 v13, v90
	v_mov_b32_e32 v91, v11
	v_pk_mul_f32 v[76:77], v[12:13], v[76:77] op_sel_hi:[1,0] neg_lo:[0,1] neg_hi:[0,1]
	v_pk_add_f32 v[42:43], v[20:21], v[30:31] neg_lo:[0,1] neg_hi:[0,1]
	v_pk_fma_f32 v[74:75], v[90:91], v[74:75], v[76:77] op_sel_hi:[1,0,1] neg_lo:[0,1,0] neg_hi:[0,1,0]
	s_waitcnt vmcnt(1)
	v_sub_f32_e32 v76, v64, v70
	v_mov_b32_e32 v13, v76
	v_mov_b32_e32 v77, v11
	v_pk_mul_f32 v[90:91], v[12:13], v[40:41] op_sel_hi:[1,0] neg_lo:[0,1] neg_hi:[0,1]
	v_pk_add_f32 v[32:33], v[46:47], v[32:33]
	v_pk_fma_f32 v[76:77], v[76:77], v[36:37], v[90:91] op_sel_hi:[1,0,1] neg_lo:[0,1,0] neg_hi:[0,1,0]
	s_waitcnt vmcnt(0)
	v_sub_f32_e32 v90, v65, v71
	v_mov_b32_e32 v13, v90
	v_pk_mul_f32 v[78:79], v[12:13], v[78:79] op_sel_hi:[1,0] neg_lo:[0,1] neg_hi:[0,1]
	v_mov_b32_e32 v13, v43
	v_mov_b32_e32 v46, v42
	v_pk_add_f32 v[20:21], v[20:21], v[30:31]
	v_mov_b32_e32 v30, v43
	v_mov_b32_e32 v31, v11
	v_pk_mul_f32 v[42:43], v[12:13], v[40:41] op_sel_hi:[1,0] neg_lo:[0,1] neg_hi:[0,1]
	v_pk_add_f32 v[34:35], v[62:63], v[38:39]
	v_pk_fma_f32 v[62:63], v[30:31], v[36:37], v[42:43] op_sel_hi:[1,0,1]
	v_pk_add_f32 v[30:31], v[26:27], v[32:33] neg_lo:[0,1] neg_hi:[0,1]
	v_pk_add_f32 v[24:25], v[24:25], v[66:67]
	v_mov_b32_e32 v13, v30
	v_mov_b32_e32 v42, v30
	v_pk_mul_f32 v[48:49], v[12:13], v[28:29] op_sel_hi:[1,0] neg_lo:[0,1] neg_hi:[0,1]
	v_pk_add_f32 v[26:27], v[26:27], v[32:33]
	v_mov_b32_e32 v32, v31
	v_mov_b32_e32 v33, v11
	v_mov_b32_e32 v13, v31
	v_pk_add_f32 v[30:31], v[24:25], v[34:35] neg_lo:[0,1] neg_hi:[0,1]
	v_pk_add_f32 v[22:23], v[22:23], v[68:69]
	v_pk_add_f32 v[38:39], v[64:65], v[70:71]
	v_pk_mul_f32 v[32:33], v[32:33], v[40:41] op_sel_hi:[1,0]
	v_pk_add_f32 v[24:25], v[24:25], v[34:35]
	v_mov_b32_e32 v34, v31
	v_mov_b32_e32 v35, v11
	v_pk_fma_f32 v[32:33], v[12:13], v[36:37], v[32:33] op_sel_hi:[1,0,1] neg_lo:[0,1,0] neg_hi:[0,1,0]
	v_xor_b32_e32 v67, 0x80000000, v30
	v_pk_mul_f32 v[34:35], v[34:35], v[40:41] op_sel_hi:[1,0] neg_lo:[0,1] neg_hi:[0,1]
	v_mov_b32_e32 v13, v31
	v_pk_add_f32 v[30:31], v[22:23], v[38:39] neg_lo:[0,1] neg_hi:[0,1]
	v_mov_b32_e32 v43, v11
	v_pk_fma_f32 v[68:69], v[12:13], v[36:37], v[34:35] op_sel_hi:[1,0,1] neg_lo:[0,1,0] neg_hi:[0,1,0]
	v_mov_b32_e32 v13, v30
	v_pk_fma_f32 v[64:65], v[42:43], v[28:29], v[48:49] op_sel_hi:[1,0,1]
	v_mov_b32_e32 v34, v30
	v_mov_b32_e32 v35, v11
	v_pk_mul_f32 v[42:43], v[12:13], v[28:29] op_sel_hi:[1,0] neg_lo:[0,1] neg_hi:[0,1]
	v_mov_b32_e32 v13, v31
	v_pk_fma_f32 v[70:71], v[34:35], v[28:29], v[42:43] op_sel_hi:[1,0,1] neg_lo:[0,1,0] neg_hi:[0,1,0]
	v_mov_b32_e32 v34, v31
	v_pk_mul_f32 v[30:31], v[12:13], v[40:41] op_sel_hi:[1,0] neg_lo:[0,1] neg_hi:[0,1]
	v_pk_add_f32 v[22:23], v[22:23], v[38:39]
	v_pk_fma_f32 v[38:39], v[34:35], v[36:37], v[30:31] op_sel_hi:[1,0,1] neg_lo:[0,1,0] neg_hi:[0,1,0]
	v_pk_add_f32 v[30:31], v[20:21], v[24:25] neg_lo:[0,1] neg_hi:[0,1]
	v_pk_add_f32 v[20:21], v[20:21], v[24:25]
	v_mov_b32_e32 v13, v31
	v_mov_b32_e32 v42, v30
	v_mov_b32_e32 v24, v31
	v_mov_b32_e32 v25, v11
	v_pk_mul_f32 v[30:31], v[12:13], v[28:29] op_sel_hi:[1,0] neg_lo:[0,1] neg_hi:[0,1]
	v_mov_b32_e32 v91, v11
	v_pk_fma_f32 v[30:31], v[24:25], v[28:29], v[30:31] op_sel_hi:[1,0,1]
	v_pk_add_f32 v[24:25], v[26:27], v[22:23] neg_lo:[0,1] neg_hi:[0,1]
	v_pk_fma_f32 v[72:73], v[90:91], v[72:73], v[78:79] op_sel_hi:[1,0,1] neg_lo:[0,1,0] neg_hi:[0,1,0]
	v_mov_b32_e32 v13, v25
	v_xor_b32_e32 v79, 0x80000000, v24
	v_pk_add_f32 v[22:23], v[26:27], v[22:23]
	v_mov_b32_e32 v26, v25
	v_mov_b32_e32 v27, v11
	v_pk_mul_f32 v[24:25], v[12:13], v[28:29] op_sel_hi:[1,0] neg_lo:[0,1] neg_hi:[0,1]
	v_pk_add_f32 v[34:35], v[20:21], v[22:23]
	v_pk_fma_f32 v[26:27], v[26:27], v[28:29], v[24:25] op_sel_hi:[1,0,1] neg_lo:[0,1,0] neg_hi:[0,1,0]
	v_pk_add_f32 v[24:25], v[20:21], v[22:23] neg_lo:[0,1] neg_hi:[0,1]
	v_mov_b32_e32 v43, v11
	v_pk_add_f32 v[20:21], v[24:25], 0 neg_lo:[1,1] neg_hi:[1,1]
	v_mov_b32_e32 v78, v11
	v_mov_b32_e32 v90, v24
	v_mov_b32_e32 v20, v11
	v_pk_add_f32 v[48:49], v[90:91], v[20:21]
	v_pk_add_f32 v[24:25], v[90:91], v[20:21] neg_lo:[0,1] neg_hi:[0,1]
	v_pk_add_f32 v[20:21], v[42:43], v[78:79]
	v_pk_add_f32 v[22:23], v[42:43], v[78:79] neg_lo:[0,1] neg_hi:[0,1]
	v_pk_add_f32 v[42:43], v[30:31], v[26:27]
	v_pk_add_f32 v[26:27], v[30:31], v[26:27] neg_lo:[0,1] neg_hi:[0,1]
	v_mov_b32_e32 v47, v11
	v_mov_b32_e32 v66, v11
	v_xor_b32_e32 v79, 0x80000000, v26
	v_mov_b32_e32 v78, v27
	v_pk_add_f32 v[26:27], v[62:63], v[68:69]
	v_pk_add_f32 v[62:63], v[62:63], v[68:69] neg_lo:[0,1] neg_hi:[0,1]
	v_pk_add_f32 v[90:91], v[20:21], v[42:43]
	v_pk_add_f32 v[30:31], v[20:21], v[42:43] neg_lo:[0,1] neg_hi:[0,1]
	v_pk_add_f32 v[42:43], v[22:23], v[78:79]
	v_pk_add_f32 v[20:21], v[22:23], v[78:79] neg_lo:[0,1] neg_hi:[0,1]
	v_pk_add_f32 v[22:23], v[46:47], v[66:67]
	v_pk_add_f32 v[46:47], v[46:47], v[66:67] neg_lo:[0,1] neg_hi:[0,1]
	v_pk_mul_f32 v[66:67], v[28:29], v[62:63] op_sel:[0,1] op_sel_hi:[0,0] neg_lo:[1,1] neg_hi:[1,0]
	v_pk_fma_f32 v[66:67], v[28:29], v[62:63], v[66:67] op_sel_hi:[0,1,1]
	v_pk_add_f32 v[62:63], v[64:65], v[70:71]
	v_pk_add_f32 v[64:65], v[64:65], v[70:71] neg_lo:[0,1] neg_hi:[0,1]
	v_mov_b32_e32 v80, v11
	v_xor_b32_e32 v69, 0x80000000, v64
	v_mov_b32_e32 v68, v65
	v_pk_add_f32 v[64:65], v[32:33], v[38:39]
	v_pk_add_f32 v[32:33], v[32:33], v[38:39] neg_lo:[0,1] neg_hi:[0,1]
	v_pk_add_f32 v[78:79], v[44:45], v[82:83]
	v_pk_mul_f32 v[38:39], v[28:29], v[32:33] op_sel:[0,1] op_sel_hi:[0,0] neg_lo:[1,1] neg_hi:[1,0]
	v_pk_fma_f32 v[32:33], v[28:29], v[32:33], v[38:39] op_sel_hi:[0,1,1] neg_lo:[1,0,0] neg_hi:[1,0,0]
	v_pk_add_f32 v[38:39], v[22:23], v[62:63]
	v_pk_add_f32 v[22:23], v[22:23], v[62:63] neg_lo:[0,1] neg_hi:[0,1]
	v_pk_add_f32 v[62:63], v[26:27], v[64:65]
	v_pk_add_f32 v[26:27], v[26:27], v[64:65] neg_lo:[0,1] neg_hi:[0,1]
	v_pk_add_f32 v[70:71], v[38:39], v[62:63]
	v_pk_add_f32 v[38:39], v[38:39], v[62:63] neg_lo:[0,1] neg_hi:[0,1]
	v_pk_add_f32 v[62:63], v[22:23], v[26:27] op_sel:[0,1] op_sel_hi:[1,0] neg_hi:[0,1]
	v_pk_add_f32 v[26:27], v[22:23], v[26:27] op_sel:[0,1] op_sel_hi:[1,0] neg_lo:[0,1]
	v_pk_add_f32 v[22:23], v[46:47], v[68:69]
	v_pk_add_f32 v[64:65], v[46:47], v[68:69] neg_lo:[0,1] neg_hi:[0,1]
	v_pk_add_f32 v[46:47], v[66:67], v[32:33]
	v_pk_add_f32 v[32:33], v[66:67], v[32:33] neg_lo:[0,1] neg_hi:[0,1]
	v_pk_add_f32 v[44:45], v[44:45], v[82:83] neg_lo:[0,1] neg_hi:[0,1]
	v_xor_b32_e32 v67, 0x80000000, v32
	v_mov_b32_e32 v66, v33
	v_pk_add_f32 v[68:69], v[22:23], v[46:47]
	v_pk_add_f32 v[32:33], v[22:23], v[46:47] neg_lo:[0,1] neg_hi:[0,1]
	v_pk_add_f32 v[46:47], v[64:65], v[66:67]
	v_pk_add_f32 v[22:23], v[64:65], v[66:67] neg_lo:[0,1] neg_hi:[0,1]
	v_pk_add_f32 v[64:65], v[10:11], v[80:81]
	v_pk_add_f32 v[66:67], v[10:11], v[80:81] neg_lo:[0,1] neg_hi:[0,1]
	v_pk_mul_f32 v[80:81], v[40:41], v[44:45] op_sel:[0,1] op_sel_hi:[0,0] neg_lo:[1,1] neg_hi:[1,0]
	v_pk_fma_f32 v[44:45], v[36:37], v[44:45], v[80:81] op_sel_hi:[0,1,1]
	v_pk_add_f32 v[80:81], v[50:51], v[84:85]
	v_pk_add_f32 v[50:51], v[50:51], v[84:85] neg_lo:[0,1] neg_hi:[0,1]
	v_add_f32_e32 v10, v34, v35
	v_pk_mul_f32 v[82:83], v[28:29], v[50:51] op_sel:[0,1] op_sel_hi:[0,0] neg_lo:[1,1] neg_hi:[1,0]
	v_pk_fma_f32 v[82:83], v[28:29], v[50:51], v[82:83] op_sel_hi:[0,1,1]
	v_pk_add_f32 v[50:51], v[54:55], v[86:87]
	v_pk_add_f32 v[54:55], v[54:55], v[86:87] neg_lo:[0,1] neg_hi:[0,1]
	v_pk_fma_f32 v[16:17], v[10:11], s[94:95], v[16:17] op_sel_hi:[0,1,1]
	v_pk_mul_f32 v[84:85], v[36:37], v[54:55] op_sel:[0,1] op_sel_hi:[0,0] neg_lo:[1,1] neg_hi:[1,0]
	v_pk_fma_f32 v[84:85], v[40:41], v[54:55], v[84:85] op_sel_hi:[0,1,1]
	v_pk_add_f32 v[54:55], v[56:57], v[88:89]
	v_pk_add_f32 v[56:57], v[56:57], v[88:89] neg_lo:[0,1] neg_hi:[0,1]
	v_lshl_add_u32 v13, v15, 3, 0
	v_xor_b32_e32 v87, 0x80000000, v56
	v_mov_b32_e32 v86, v57
	v_pk_add_f32 v[56:57], v[60:61], v[74:75]
	v_pk_add_f32 v[60:61], v[60:61], v[74:75] neg_lo:[0,1] neg_hi:[0,1]
	ds_write_b64 v13, v[16:17]
	v_pk_mul_f32 v[74:75], v[36:37], v[60:61] op_sel:[0,1] op_sel_hi:[0,0] neg_lo:[1,1] neg_hi:[1,0]
	v_pk_fma_f32 v[60:61], v[40:41], v[60:61], v[74:75] op_sel_hi:[0,1,1] neg_lo:[1,0,0] neg_hi:[1,0,0]
	v_pk_add_f32 v[74:75], v[58:59], v[76:77]
	v_pk_add_f32 v[58:59], v[58:59], v[76:77] neg_lo:[0,1] neg_hi:[0,1]
	v_pk_fma_f32 v[16:17], v[178:179], s[90:91], v[178:179] op_sel:[1,0,0] op_sel_hi:[0,1,1]
	v_pk_mul_f32 v[76:77], v[28:29], v[58:59] op_sel:[0,1] op_sel_hi:[0,0] neg_lo:[1,1] neg_hi:[1,0]
	v_pk_fma_f32 v[58:59], v[28:29], v[58:59], v[76:77] op_sel_hi:[0,1,1] neg_lo:[1,0,0] neg_hi:[1,0,0]
	v_pk_add_f32 v[76:77], v[52:53], v[72:73]
	v_pk_add_f32 v[52:53], v[52:53], v[72:73] neg_lo:[0,1] neg_hi:[0,1]
	s_nop 0
	v_pk_mul_f32 v[40:41], v[40:41], v[52:53] op_sel:[0,1] op_sel_hi:[0,0] neg_lo:[1,1] neg_hi:[1,0]
	v_pk_fma_f32 v[52:53], v[36:37], v[52:53], v[40:41] op_sel_hi:[0,1,1] neg_lo:[1,0,0] neg_hi:[1,0,0]
	v_pk_add_f32 v[36:37], v[64:65], v[54:55]
	v_pk_add_f32 v[64:65], v[64:65], v[54:55] neg_lo:[0,1] neg_hi:[0,1]
	v_pk_add_f32 v[54:55], v[78:79], v[56:57] neg_lo:[0,1] neg_hi:[0,1]
	v_pk_add_f32 v[40:41], v[56:57], v[78:79]
	v_pk_mul_f32 v[56:57], v[28:29], v[54:55] op_sel:[0,1] op_sel_hi:[0,0] neg_lo:[1,1] neg_hi:[1,0]
	v_pk_add_f32 v[72:73], v[80:81], v[74:75] neg_lo:[0,1] neg_hi:[0,1]
	v_pk_fma_f32 v[56:57], v[28:29], v[54:55], v[56:57] op_sel_hi:[0,1,1]
	v_pk_add_f32 v[54:55], v[80:81], v[74:75]
	v_xor_b32_e32 v75, 0x80000000, v72
	v_mov_b32_e32 v74, v73
	v_pk_add_f32 v[72:73], v[50:51], v[76:77]
	v_pk_add_f32 v[50:51], v[50:51], v[76:77] neg_lo:[0,1] neg_hi:[0,1]
	s_nop 0
	v_pk_mul_f32 v[76:77], v[28:29], v[50:51] op_sel:[0,1] op_sel_hi:[0,0] neg_lo:[1,1] neg_hi:[1,0]
	v_pk_fma_f32 v[50:51], v[28:29], v[50:51], v[76:77] op_sel_hi:[0,1,1] neg_lo:[1,0,0] neg_hi:[1,0,0]
	v_pk_add_f32 v[76:77], v[36:37], v[54:55]
	v_pk_add_f32 v[36:37], v[36:37], v[54:55] neg_lo:[0,1] neg_hi:[0,1]
	v_pk_add_f32 v[54:55], v[40:41], v[72:73]
	v_pk_add_f32 v[40:41], v[40:41], v[72:73] neg_lo:[0,1] neg_hi:[0,1]
	v_pk_add_f32 v[78:79], v[76:77], v[54:55]
	v_pk_add_f32 v[54:55], v[76:77], v[54:55] neg_lo:[0,1] neg_hi:[0,1]
	v_pk_add_f32 v[76:77], v[36:37], v[40:41] op_sel:[0,1] op_sel_hi:[1,0] neg_hi:[0,1]
	v_pk_add_f32 v[40:41], v[36:37], v[40:41] op_sel:[0,1] op_sel_hi:[1,0] neg_lo:[0,1]
	v_pk_add_f32 v[72:73], v[56:57], v[50:51]
	v_pk_add_f32 v[50:51], v[56:57], v[50:51] neg_lo:[0,1] neg_hi:[0,1]
	v_pk_add_f32 v[36:37], v[64:65], v[74:75]
	v_pk_add_f32 v[64:65], v[64:65], v[74:75] neg_lo:[0,1] neg_hi:[0,1]
	v_xor_b32_e32 v57, 0x80000000, v50
	v_mov_b32_e32 v56, v51
	v_pk_add_f32 v[74:75], v[36:37], v[72:73]
	v_pk_add_f32 v[50:51], v[36:37], v[72:73] neg_lo:[0,1] neg_hi:[0,1]
	v_pk_add_f32 v[72:73], v[64:65], v[56:57]
	v_pk_add_f32 v[36:37], v[64:65], v[56:57] neg_lo:[0,1] neg_hi:[0,1]
	v_pk_add_f32 v[56:57], v[66:67], v[86:87]
	v_pk_add_f32 v[64:65], v[66:67], v[86:87] neg_lo:[0,1] neg_hi:[0,1]
	v_pk_add_f32 v[66:67], v[60:61], v[44:45]
	v_pk_add_f32 v[44:45], v[44:45], v[60:61] neg_lo:[0,1] neg_hi:[0,1]
	s_nop 0
	v_pk_mul_f32 v[60:61], v[28:29], v[44:45] op_sel:[0,1] op_sel_hi:[0,0] neg_lo:[1,1] neg_hi:[1,0]
	v_pk_fma_f32 v[60:61], v[28:29], v[44:45], v[60:61] op_sel_hi:[0,1,1]
	v_pk_add_f32 v[44:45], v[82:83], v[58:59]
	v_pk_add_f32 v[58:59], v[82:83], v[58:59] neg_lo:[0,1] neg_hi:[0,1]
	s_nop 0
	v_xor_b32_e32 v81, 0x80000000, v58
	v_mov_b32_e32 v80, v59
	v_pk_add_f32 v[58:59], v[84:85], v[52:53]
	v_pk_add_f32 v[52:53], v[84:85], v[52:53] neg_lo:[0,1] neg_hi:[0,1]
	s_nop 0
	v_pk_mul_f32 v[82:83], v[28:29], v[52:53] op_sel:[0,1] op_sel_hi:[0,0] neg_lo:[1,1] neg_hi:[1,0]
	v_pk_fma_f32 v[28:29], v[28:29], v[52:53], v[82:83] op_sel_hi:[0,1,1] neg_lo:[1,0,0] neg_hi:[1,0,0]
	v_pk_add_f32 v[52:53], v[56:57], v[44:45]
	v_pk_add_f32 v[44:45], v[56:57], v[44:45] neg_lo:[0,1] neg_hi:[0,1]
	v_pk_add_f32 v[56:57], v[66:67], v[58:59]
	v_pk_add_f32 v[58:59], v[66:67], v[58:59] neg_lo:[0,1] neg_hi:[0,1]
	s_nop 0
	v_pk_add_f32 v[82:83], v[44:45], v[58:59] op_sel:[0,1] op_sel_hi:[1,0] neg_hi:[0,1]
	v_pk_add_f32 v[44:45], v[44:45], v[58:59] op_sel:[0,1] op_sel_hi:[1,0] neg_lo:[0,1]
	v_pk_add_f32 v[66:67], v[60:61], v[28:29]
	v_pk_add_f32 v[28:29], v[60:61], v[28:29] neg_lo:[0,1] neg_hi:[0,1]
	v_pk_add_f32 v[58:59], v[52:53], v[56:57]
	v_pk_add_f32 v[56:57], v[52:53], v[56:57] neg_lo:[0,1] neg_hi:[0,1]
	v_pk_add_f32 v[52:53], v[64:65], v[80:81]
	v_pk_add_f32 v[64:65], v[64:65], v[80:81] neg_lo:[0,1] neg_hi:[0,1]
	v_pk_add_f32 v[80:81], v[52:53], v[66:67]
	v_pk_add_f32 v[52:53], v[52:53], v[66:67] neg_lo:[0,1] neg_hi:[0,1]
	v_pk_add_f32 v[66:67], v[64:65], v[28:29] op_sel:[0,1] op_sel_hi:[1,0] neg_hi:[0,1]
	v_pk_add_f32 v[28:29], v[64:65], v[28:29] op_sel:[0,1] op_sel_hi:[1,0] neg_lo:[0,1]
	v_pk_mul_f32 v[60:61], v[16:17], v[78:79] op_sel:[1,1] op_sel_hi:[0,1] neg_lo:[0,1]
	v_pk_fma_f32 v[60:61], v[16:17], v[78:79], v[60:61] op_sel_hi:[1,0,1]
	ds_write_b64 v13, v[60:61] offset:4224
	v_pk_mul_f32 v[60:61], v[178:179], v[16:17] op_sel:[1,1] op_sel_hi:[0,1] neg_lo:[0,1]
	v_pk_fma_f32 v[16:17], v[178:179], v[16:17], v[60:61] op_sel_hi:[1,0,1]
	s_nop 0
	v_pk_mul_f32 v[60:61], v[16:17], v[70:71] op_sel:[1,1] op_sel_hi:[0,1] neg_lo:[0,1]
	v_pk_fma_f32 v[60:61], v[16:17], v[70:71], v[60:61] op_sel_hi:[1,0,1]
	ds_write_b64 v13, v[60:61] offset:8448
	v_pk_mul_f32 v[60:61], v[178:179], v[16:17] op_sel:[1,1] op_sel_hi:[0,1] neg_lo:[0,1]
	v_pk_fma_f32 v[16:17], v[178:179], v[16:17], v[60:61] op_sel_hi:[1,0,1]
	s_nop 0
	v_pk_mul_f32 v[60:61], v[16:17], v[58:59] op_sel:[1,1] op_sel_hi:[0,1] neg_lo:[0,1]
	v_pk_fma_f32 v[58:59], v[16:17], v[58:59], v[60:61] op_sel_hi:[1,0,1]
	ds_write_b64 v13, v[58:59] offset:12672
	v_pk_mul_f32 v[58:59], v[178:179], v[16:17] op_sel:[1,1] op_sel_hi:[0,1] neg_lo:[0,1]
	v_pk_fma_f32 v[16:17], v[178:179], v[16:17], v[58:59] op_sel_hi:[1,0,1]
	s_nop 0
	v_pk_mul_f32 v[58:59], v[90:91], v[16:17] op_sel:[1,1] op_sel_hi:[1,0] neg_lo:[1,0]
	s_nop 0
	v_pk_fma_f32 v[58:59], v[90:91], v[16:17], v[58:59] op_sel_hi:[0,1,1]
	ds_write_b64 v13, v[58:59] offset:16896
	v_pk_mul_f32 v[58:59], v[178:179], v[16:17] op_sel:[1,1] op_sel_hi:[0,1] neg_lo:[0,1]
	v_pk_fma_f32 v[16:17], v[178:179], v[16:17], v[58:59] op_sel_hi:[1,0,1]
	s_nop 0
	v_pk_mul_f32 v[58:59], v[16:17], v[74:75] op_sel:[1,1] op_sel_hi:[0,1] neg_lo:[0,1]
	v_pk_fma_f32 v[58:59], v[16:17], v[74:75], v[58:59] op_sel_hi:[1,0,1]
	ds_write_b64 v13, v[58:59] offset:21120
	v_pk_mul_f32 v[58:59], v[178:179], v[16:17] op_sel:[1,1] op_sel_hi:[0,1] neg_lo:[0,1]
	v_pk_fma_f32 v[16:17], v[178:179], v[16:17], v[58:59] op_sel_hi:[1,0,1]
	s_nop 0
	v_pk_mul_f32 v[58:59], v[68:69], v[16:17] op_sel:[1,1] op_sel_hi:[1,0] neg_lo:[1,0]
	s_nop 0
	v_pk_fma_f32 v[58:59], v[68:69], v[16:17], v[58:59] op_sel_hi:[0,1,1]
	ds_write_b64 v13, v[58:59] offset:25344
	v_pk_mul_f32 v[58:59], v[178:179], v[16:17] op_sel:[1,1] op_sel_hi:[0,1] neg_lo:[0,1]
	v_pk_fma_f32 v[16:17], v[178:179], v[16:17], v[58:59] op_sel_hi:[1,0,1]
	s_nop 0
	v_pk_mul_f32 v[58:59], v[80:81], v[16:17] op_sel:[1,1] op_sel_hi:[1,0] neg_lo:[1,0]
	s_nop 0
	v_pk_fma_f32 v[58:59], v[80:81], v[16:17], v[58:59] op_sel_hi:[0,1,1]
	ds_write_b64 v13, v[58:59] offset:29568
	v_pk_mul_f32 v[58:59], v[178:179], v[16:17] op_sel:[1,1] op_sel_hi:[0,1] neg_lo:[0,1]
	v_pk_fma_f32 v[16:17], v[178:179], v[16:17], v[58:59] op_sel_hi:[1,0,1]
	s_nop 0
	v_pk_mul_f32 v[58:59], v[48:49], v[16:17] op_sel:[1,1] op_sel_hi:[1,0] neg_lo:[1,0]
	s_nop 0
	v_pk_fma_f32 v[48:49], v[48:49], v[16:17], v[58:59] op_sel_hi:[0,1,1]
	ds_write_b64 v13, v[48:49] offset:33792
	v_pk_mul_f32 v[48:49], v[178:179], v[16:17] op_sel:[1,1] op_sel_hi:[0,1] neg_lo:[0,1]
	v_pk_fma_f32 v[16:17], v[178:179], v[16:17], v[48:49] op_sel_hi:[1,0,1]
	s_nop 0
	v_pk_mul_f32 v[48:49], v[76:77], v[16:17] op_sel:[1,1] op_sel_hi:[1,0] neg_lo:[1,0]
	s_nop 0
	v_pk_fma_f32 v[48:49], v[76:77], v[16:17], v[48:49] op_sel_hi:[0,1,1]
	ds_write_b64 v13, v[48:49] offset:38016
	v_pk_mul_f32 v[48:49], v[178:179], v[16:17] op_sel:[1,1] op_sel_hi:[0,1] neg_lo:[0,1]
	v_pk_fma_f32 v[16:17], v[178:179], v[16:17], v[48:49] op_sel_hi:[1,0,1]
	s_nop 0
	v_pk_mul_f32 v[48:49], v[62:63], v[16:17] op_sel:[1,1] op_sel_hi:[1,0] neg_lo:[1,0]
	s_nop 0
	v_pk_fma_f32 v[48:49], v[62:63], v[16:17], v[48:49] op_sel_hi:[0,1,1]
	ds_write_b64 v13, v[48:49] offset:42240
	v_pk_mul_f32 v[48:49], v[178:179], v[16:17] op_sel:[1,1] op_sel_hi:[0,1] neg_lo:[0,1]
	v_pk_fma_f32 v[16:17], v[178:179], v[16:17], v[48:49] op_sel_hi:[1,0,1]
	s_nop 0
	v_pk_mul_f32 v[48:49], v[82:83], v[16:17] op_sel:[1,1] op_sel_hi:[1,0] neg_lo:[1,0]
	s_nop 0
	v_pk_fma_f32 v[48:49], v[82:83], v[16:17], v[48:49] op_sel_hi:[0,1,1]
	ds_write_b64 v13, v[48:49] offset:46464
	v_pk_mul_f32 v[48:49], v[178:179], v[16:17] op_sel:[1,1] op_sel_hi:[0,1] neg_lo:[0,1]
	v_pk_fma_f32 v[16:17], v[178:179], v[16:17], v[48:49] op_sel_hi:[1,0,1]
	s_nop 0
	v_pk_mul_f32 v[48:49], v[42:43], v[16:17] op_sel:[1,1] op_sel_hi:[1,0] neg_lo:[1,0]
	s_nop 0
	v_pk_fma_f32 v[42:43], v[42:43], v[16:17], v[48:49] op_sel_hi:[0,1,1]
	ds_write_b64 v13, v[42:43] offset:50688
	v_pk_mul_f32 v[42:43], v[178:179], v[16:17] op_sel:[1,1] op_sel_hi:[0,1] neg_lo:[0,1]
	v_pk_fma_f32 v[16:17], v[178:179], v[16:17], v[42:43] op_sel_hi:[1,0,1]
	s_nop 0
	v_pk_mul_f32 v[42:43], v[72:73], v[16:17] op_sel:[1,1] op_sel_hi:[1,0] neg_lo:[1,0]
	s_nop 0
	v_pk_fma_f32 v[42:43], v[72:73], v[16:17], v[42:43] op_sel_hi:[0,1,1]
	ds_write_b64 v13, v[42:43] offset:54912
	v_pk_mul_f32 v[42:43], v[178:179], v[16:17] op_sel:[1,1] op_sel_hi:[0,1] neg_lo:[0,1]
	v_pk_fma_f32 v[16:17], v[178:179], v[16:17], v[42:43] op_sel_hi:[1,0,1]
	s_nop 0
	v_pk_mul_f32 v[42:43], v[46:47], v[16:17] op_sel:[1,1] op_sel_hi:[1,0] neg_lo:[1,0]
	s_nop 0
	v_pk_fma_f32 v[42:43], v[46:47], v[16:17], v[42:43] op_sel_hi:[0,1,1]
	ds_write_b64 v13, v[42:43] offset:59136
	v_pk_mul_f32 v[42:43], v[178:179], v[16:17] op_sel:[1,1] op_sel_hi:[0,1] neg_lo:[0,1]
	v_pk_fma_f32 v[16:17], v[178:179], v[16:17], v[42:43] op_sel_hi:[1,0,1]
	s_nop 0
	v_pk_mul_f32 v[42:43], v[66:67], v[16:17] op_sel:[1,1] op_sel_hi:[1,0] neg_lo:[1,0]
	s_nop 0
	v_pk_fma_f32 v[42:43], v[66:67], v[16:17], v[42:43] op_sel_hi:[0,1,1]
	ds_write_b64 v13, v[42:43] offset:63360
	v_pk_mul_f32 v[42:43], v[178:179], v[16:17] op_sel:[1,1] op_sel_hi:[0,1] neg_lo:[0,1]
	v_pk_fma_f32 v[16:17], v[178:179], v[16:17], v[42:43] op_sel_hi:[1,0,1]
	v_sub_f32_e32 v10, v34, v35
	v_pk_mul_f32 v[34:35], v[16:17], s[44:45]
	s_nop 0
	v_pk_fma_f32 v[34:35], v[10:11], v[16:17], v[34:35] op_sel:[0,0,1] op_sel_hi:[0,1,0]
	v_add_u32_e32 v10, 0x10800, v13
	ds_write_b64 v10, v[34:35]
	v_pk_mul_f32 v[34:35], v[178:179], v[16:17] op_sel:[1,1] op_sel_hi:[0,1] neg_lo:[0,1]
	v_pk_fma_f32 v[16:17], v[178:179], v[16:17], v[34:35] op_sel_hi:[1,0,1]
	s_nop 0
	v_pk_mul_f32 v[34:35], v[54:55], v[16:17] op_sel:[1,1] op_sel_hi:[1,0] neg_lo:[1,0]
	v_add_u32_e32 v10, 0x11880, v13
	v_pk_fma_f32 v[34:35], v[54:55], v[16:17], v[34:35] op_sel_hi:[0,1,1]
	ds_write_b64 v10, v[34:35]
	v_pk_mul_f32 v[34:35], v[178:179], v[16:17] op_sel:[1,1] op_sel_hi:[0,1] neg_lo:[0,1]
	v_pk_fma_f32 v[16:17], v[178:179], v[16:17], v[34:35] op_sel_hi:[1,0,1]
	s_nop 0
	v_pk_mul_f32 v[34:35], v[38:39], v[16:17] op_sel:[1,1] op_sel_hi:[1,0] neg_lo:[1,0]
	v_add_u32_e32 v10, 0x12900, v13
	v_pk_fma_f32 v[34:35], v[38:39], v[16:17], v[34:35] op_sel_hi:[0,1,1]
	ds_write_b64 v10, v[34:35]
	v_pk_mul_f32 v[34:35], v[178:179], v[16:17] op_sel:[1,1] op_sel_hi:[0,1] neg_lo:[0,1]
	v_pk_fma_f32 v[16:17], v[178:179], v[16:17], v[34:35] op_sel_hi:[1,0,1]
	s_nop 0
	v_pk_mul_f32 v[34:35], v[56:57], v[16:17] op_sel:[1,1] op_sel_hi:[1,0] neg_lo:[1,0]
	v_add_u32_e32 v10, 0x13980, v13
	v_pk_fma_f32 v[34:35], v[56:57], v[16:17], v[34:35] op_sel_hi:[0,1,1]
	ds_write_b64 v10, v[34:35]
	v_pk_mul_f32 v[34:35], v[178:179], v[16:17] op_sel:[1,1] op_sel_hi:[0,1] neg_lo:[0,1]
	v_pk_fma_f32 v[16:17], v[178:179], v[16:17], v[34:35] op_sel_hi:[1,0,1]
	s_nop 0
	v_pk_mul_f32 v[34:35], v[30:31], v[16:17] op_sel:[1,1] op_sel_hi:[1,0] neg_lo:[1,0]
	v_add_u32_e32 v10, 0x14a00, v13
	v_pk_fma_f32 v[30:31], v[30:31], v[16:17], v[34:35] op_sel_hi:[0,1,1]
	ds_write_b64 v10, v[30:31]
	v_pk_mul_f32 v[30:31], v[178:179], v[16:17] op_sel:[1,1] op_sel_hi:[0,1] neg_lo:[0,1]
	v_pk_fma_f32 v[16:17], v[178:179], v[16:17], v[30:31] op_sel_hi:[1,0,1]
	s_nop 0
	v_pk_mul_f32 v[30:31], v[50:51], v[16:17] op_sel:[1,1] op_sel_hi:[1,0] neg_lo:[1,0]
	v_add_u32_e32 v10, 0x15a80, v13
	v_pk_fma_f32 v[30:31], v[50:51], v[16:17], v[30:31] op_sel_hi:[0,1,1]
	ds_write_b64 v10, v[30:31]
	v_pk_mul_f32 v[30:31], v[178:179], v[16:17] op_sel:[1,1] op_sel_hi:[0,1] neg_lo:[0,1]
	v_pk_fma_f32 v[16:17], v[178:179], v[16:17], v[30:31] op_sel_hi:[1,0,1]
	s_nop 0
	v_pk_mul_f32 v[30:31], v[32:33], v[16:17] op_sel:[1,1] op_sel_hi:[1,0] neg_lo:[1,0]
	v_add_u32_e32 v10, 0x16b00, v13
	v_pk_fma_f32 v[30:31], v[32:33], v[16:17], v[30:31] op_sel_hi:[0,1,1]
	ds_write_b64 v10, v[30:31]
	v_pk_mul_f32 v[30:31], v[178:179], v[16:17] op_sel:[1,1] op_sel_hi:[0,1] neg_lo:[0,1]
	v_pk_fma_f32 v[16:17], v[178:179], v[16:17], v[30:31] op_sel_hi:[1,0,1]
	s_nop 0
	v_pk_mul_f32 v[30:31], v[52:53], v[16:17] op_sel:[1,1] op_sel_hi:[1,0] neg_lo:[1,0]
	v_add_u32_e32 v10, 0x17b80, v13
	v_pk_fma_f32 v[30:31], v[52:53], v[16:17], v[30:31] op_sel_hi:[0,1,1]
	ds_write_b64 v10, v[30:31]
	v_pk_mul_f32 v[30:31], v[178:179], v[16:17] op_sel:[1,1] op_sel_hi:[0,1] neg_lo:[0,1]
	v_pk_fma_f32 v[16:17], v[178:179], v[16:17], v[30:31] op_sel_hi:[1,0,1]
	s_nop 0
	v_pk_mul_f32 v[30:31], v[24:25], v[16:17] op_sel:[1,1] op_sel_hi:[1,0] neg_lo:[1,0]
	v_add_u32_e32 v10, 0x18c00, v13
	v_pk_fma_f32 v[24:25], v[24:25], v[16:17], v[30:31] op_sel_hi:[0,1,1]
	ds_write_b64 v10, v[24:25]
	v_pk_mul_f32 v[24:25], v[178:179], v[16:17] op_sel:[1,1] op_sel_hi:[0,1] neg_lo:[0,1]
	v_pk_fma_f32 v[16:17], v[178:179], v[16:17], v[24:25] op_sel_hi:[1,0,1]
	s_nop 0
	v_pk_mul_f32 v[24:25], v[40:41], v[16:17] op_sel:[1,1] op_sel_hi:[1,0] neg_lo:[1,0]
	v_add_u32_e32 v10, 0x19c80, v13
	v_pk_fma_f32 v[24:25], v[40:41], v[16:17], v[24:25] op_sel_hi:[0,1,1]
	ds_write_b64 v10, v[24:25]
	v_pk_mul_f32 v[24:25], v[178:179], v[16:17] op_sel:[1,1] op_sel_hi:[0,1] neg_lo:[0,1]
	v_pk_fma_f32 v[16:17], v[178:179], v[16:17], v[24:25] op_sel_hi:[1,0,1]
	s_nop 0
	v_pk_mul_f32 v[24:25], v[26:27], v[16:17] op_sel:[1,1] op_sel_hi:[1,0] neg_lo:[1,0]
	v_add_u32_e32 v10, 0x1ad00, v13
	v_pk_fma_f32 v[24:25], v[26:27], v[16:17], v[24:25] op_sel_hi:[0,1,1]
	ds_write_b64 v10, v[24:25]
	v_pk_mul_f32 v[24:25], v[178:179], v[16:17] op_sel:[1,1] op_sel_hi:[0,1] neg_lo:[0,1]
	v_pk_fma_f32 v[16:17], v[178:179], v[16:17], v[24:25] op_sel_hi:[1,0,1]
	s_nop 0
	v_pk_mul_f32 v[24:25], v[44:45], v[16:17] op_sel:[1,1] op_sel_hi:[1,0] neg_lo:[1,0]
	v_add_u32_e32 v10, 0x1bd80, v13
	v_pk_fma_f32 v[24:25], v[44:45], v[16:17], v[24:25] op_sel_hi:[0,1,1]
	ds_write_b64 v10, v[24:25]
	v_pk_mul_f32 v[24:25], v[178:179], v[16:17] op_sel:[1,1] op_sel_hi:[0,1] neg_lo:[0,1]
	v_pk_fma_f32 v[16:17], v[178:179], v[16:17], v[24:25] op_sel_hi:[1,0,1]
	s_nop 0
	v_pk_mul_f32 v[24:25], v[20:21], v[16:17] op_sel:[1,1] op_sel_hi:[1,0] neg_lo:[1,0]
	v_add_u32_e32 v10, 0x1ce00, v13
	v_pk_fma_f32 v[20:21], v[20:21], v[16:17], v[24:25] op_sel_hi:[0,1,1]
	ds_write_b64 v10, v[20:21]
	v_pk_mul_f32 v[20:21], v[178:179], v[16:17] op_sel:[1,1] op_sel_hi:[0,1] neg_lo:[0,1]
	v_pk_fma_f32 v[16:17], v[178:179], v[16:17], v[20:21] op_sel_hi:[1,0,1]
	s_nop 0
	v_pk_mul_f32 v[20:21], v[36:37], v[16:17] op_sel:[1,1] op_sel_hi:[1,0] neg_lo:[1,0]
	v_add_u32_e32 v10, 0x1de80, v13
	v_pk_fma_f32 v[20:21], v[36:37], v[16:17], v[20:21] op_sel_hi:[0,1,1]
	ds_write_b64 v10, v[20:21]
	v_pk_mul_f32 v[20:21], v[178:179], v[16:17] op_sel:[1,1] op_sel_hi:[0,1] neg_lo:[0,1]
	v_pk_fma_f32 v[16:17], v[178:179], v[16:17], v[20:21] op_sel_hi:[1,0,1]
	s_nop 0
	v_pk_mul_f32 v[20:21], v[22:23], v[16:17] op_sel:[1,1] op_sel_hi:[1,0] neg_lo:[1,0]
	v_add_u32_e32 v10, 0x1ef00, v13
	v_pk_fma_f32 v[20:21], v[22:23], v[16:17], v[20:21] op_sel_hi:[0,1,1]
	ds_write_b64 v10, v[20:21]
	v_pk_mul_f32 v[20:21], v[178:179], v[16:17] op_sel:[1,1] op_sel_hi:[0,1] neg_lo:[0,1]
	v_pk_fma_f32 v[16:17], v[178:179], v[16:17], v[20:21] op_sel_hi:[1,0,1]
	s_nop 0
	v_pk_mul_f32 v[18:19], v[28:29], v[16:17] op_sel:[1,1] op_sel_hi:[1,0] neg_lo:[1,0]
	v_add_u32_e32 v10, 0x1ff80, v13
	v_pk_fma_f32 v[16:17], v[28:29], v[16:17], v[18:19] op_sel_hi:[0,1,1]
	ds_write_b64 v10, v[16:17]
	v_mov_b32_e32 v10, v174
	v_mov_b32_e32 v13, v172
	s_waitcnt lgkmcnt(0)
	s_barrier
	v_mov_b32_e32 v16, v180
	v_add_u32_e32 v15, v13, v10
	v_lshl_add_u32 v75, v15, 3, 0
	v_xad_u32 v15, v13, 1, v10
	v_lshl_add_u32 v74, v15, 3, 0
	v_xad_u32 v15, v13, 2, v10
	v_lshl_add_u32 v73, v15, 3, 0
	v_xad_u32 v15, v13, 3, v10
	v_lshl_add_u32 v72, v15, 3, 0
	v_xad_u32 v15, v13, 4, v10
	v_lshl_add_u32 v71, v15, 3, 0
	v_xad_u32 v15, v13, 5, v10
	v_lshl_add_u32 v70, v15, 3, 0
	v_xad_u32 v15, v13, 6, v10
	v_lshl_add_u32 v69, v15, 3, 0
	v_xad_u32 v15, v13, 7, v10
	v_lshl_add_u32 v68, v15, 3, 0
	v_xad_u32 v15, v13, 8, v10
	v_lshl_add_u32 v15, v15, 3, 0
	v_add_u32_e32 v67, 0x800, v15
	v_xad_u32 v15, v13, 9, v10
	v_lshl_add_u32 v15, v15, 3, 0
	v_add_u32_e32 v66, 0x800, v15
	v_xad_u32 v15, v13, 10, v10
	v_lshl_add_u32 v15, v15, 3, 0
	v_add_u32_e32 v65, 0x800, v15
	v_xad_u32 v15, v13, 11, v10
	v_lshl_add_u32 v15, v15, 3, 0
	v_add_u32_e32 v64, 0x800, v15
	v_xad_u32 v15, v13, 12, v10
	v_mov_b32_e32 v17, v181
	v_lshl_add_u32 v15, v15, 3, 0
	ds_read2_b64 v[18:21], v75 offset1:16
	ds_read2_b64 v[40:43], v67 offset1:16
	v_add_u32_e32 v63, 0x800, v15
	v_xad_u32 v15, v13, 13, v10
	v_lshl_add_u32 v15, v15, 3, 0
	v_add_u32_e32 v62, 0x800, v15
	v_xad_u32 v15, v13, 14, v10
	v_xad_u32 v10, v13, 15, v10
	ds_read2_b64 v[22:25], v74 offset0:32 offset1:48
	ds_read2_b64 v[48:51], v66 offset0:32 offset1:48
	v_lshl_add_u32 v15, v15, 3, 0
	v_lshl_add_u32 v10, v10, 3, 0
	v_add_u32_e32 v15, 0x800, v15
	v_add_u32_e32 v13, 0x800, v10
	ds_read2_b64 v[26:29], v73 offset0:64 offset1:80
	ds_read2_b64 v[58:61], v72 offset0:96 offset1:112
	ds_read2_b64 v[76:79], v71 offset0:128 offset1:144
	ds_read2_b64 v[80:83], v70 offset0:160 offset1:176
	ds_read2_b64 v[84:87], v69 offset0:192 offset1:208
	ds_read2_b64 v[88:91], v68 offset0:224 offset1:240
	ds_read2_b64 v[54:57], v65 offset0:64 offset1:80
	ds_read2_b64 v[92:95], v64 offset0:96 offset1:112
	ds_read2_b64 v[96:99], v63 offset0:128 offset1:144
	ds_read2_b64 v[100:103], v62 offset0:160 offset1:176
	ds_read2_b64 v[104:107], v15 offset0:192 offset1:208
	ds_read2_b64 v[108:111], v13 offset0:224 offset1:240
	s_waitcnt lgkmcnt(14)
	v_pk_add_f32 v[112:113], v[18:19], v[40:41]
	v_pk_add_f32 v[40:41], v[18:19], v[40:41] neg_lo:[0,1] neg_hi:[0,1]
	v_pk_add_f32 v[18:19], v[20:21], v[42:43]
	v_pk_add_f32 v[20:21], v[20:21], v[42:43] neg_lo:[0,1] neg_hi:[0,1]
	v_mov_b32_e32 v30, v164
	v_mov_b32_e32 v32, v165
	v_mov_b32_e32 v34, v166
	v_mov_b32_e32 v10, v167
	v_mov_b32_e32 v38, v168
	v_mov_b32_e32 v36, v169
	v_mov_b32_e32 v46, v170
	v_mov_b32_e32 v31, v171
	v_pk_mul_f32 v[42:43], v[20:21], v[46:47] op_sel:[1,0] op_sel_hi:[0,0] neg_lo:[1,1] neg_hi:[0,1]
	s_nop 0
	v_pk_fma_f32 v[44:45], v[20:21], v[30:31], v[42:43] op_sel_hi:[1,0,1]
	s_waitcnt lgkmcnt(12)
	v_pk_add_f32 v[20:21], v[22:23], v[48:49]
	v_pk_add_f32 v[22:23], v[22:23], v[48:49] neg_lo:[0,1] neg_hi:[0,1]
	s_nop 0
	v_pk_mul_f32 v[42:43], v[22:23], v[36:37] op_sel:[1,0] op_sel_hi:[0,0] neg_lo:[1,1] neg_hi:[0,1]
	s_nop 0
	v_pk_fma_f32 v[48:49], v[22:23], v[32:33], v[42:43] op_sel_hi:[1,0,1]
	v_pk_add_f32 v[22:23], v[24:25], v[50:51]
	v_pk_add_f32 v[24:25], v[24:25], v[50:51] neg_lo:[0,1] neg_hi:[0,1]
	s_nop 0
	v_pk_mul_f32 v[42:43], v[24:25], v[38:39] op_sel:[1,0] op_sel_hi:[0,0] neg_lo:[1,1] neg_hi:[0,1]
	s_nop 0
	v_pk_fma_f32 v[52:53], v[24:25], v[34:35], v[42:43] op_sel_hi:[1,0,1]
	s_waitcnt lgkmcnt(5)
	v_pk_add_f32 v[24:25], v[26:27], v[54:55]
	v_pk_add_f32 v[26:27], v[26:27], v[54:55] neg_lo:[0,1] neg_hi:[0,1]
	s_nop 0
	v_pk_mul_f32 v[42:43], v[26:27], v[10:11] op_sel:[1,0] op_sel_hi:[0,0] neg_lo:[1,1] neg_hi:[0,1]
	s_nop 0
	v_pk_fma_f32 v[54:55], v[26:27], v[10:11], v[42:43] op_sel_hi:[1,0,1]
	v_pk_add_f32 v[26:27], v[28:29], v[56:57]
	v_pk_add_f32 v[28:29], v[28:29], v[56:57] neg_lo:[0,1] neg_hi:[0,1]
	s_nop 0
	v_pk_mul_f32 v[42:43], v[28:29], v[38:39] op_sel_hi:[1,0]
	s_nop 0
	v_pk_fma_f32 v[56:57], v[28:29], v[34:35], v[42:43] op_sel:[1,0,0] op_sel_hi:[0,0,1] neg_lo:[1,1,0] neg_hi:[0,1,0]
	s_waitcnt lgkmcnt(4)
	v_pk_add_f32 v[42:43], v[58:59], v[92:93] neg_lo:[0,1] neg_hi:[0,1]
	v_pk_add_f32 v[28:29], v[58:59], v[92:93]
	v_pk_mul_f32 v[50:51], v[42:43], v[36:37] op_sel_hi:[1,0]
	s_nop 0
	v_pk_fma_f32 v[58:59], v[42:43], v[32:33], v[50:51] op_sel:[1,0,0] op_sel_hi:[0,0,1] neg_lo:[1,1,0] neg_hi:[0,1,0]
	v_pk_add_f32 v[50:51], v[60:61], v[94:95] neg_lo:[0,1] neg_hi:[0,1]
	v_pk_add_f32 v[42:43], v[60:61], v[94:95]
	v_pk_mul_f32 v[60:61], v[50:51], v[46:47] op_sel_hi:[1,0]
	v_xor_b32_e32 v92, 0x80000000, v51
	v_mov_b32_e32 v93, v50
	s_waitcnt lgkmcnt(3)
	v_pk_add_f32 v[50:51], v[76:77], v[96:97]
	v_pk_add_f32 v[76:77], v[76:77], v[96:97] neg_lo:[0,1] neg_hi:[0,1]
	v_pk_fma_f32 v[60:61], v[92:93], v[30:31], v[60:61] op_sel_hi:[1,0,1] neg_lo:[0,1,0] neg_hi:[0,1,0]
	v_xor_b32_e32 v93, 0x80000000, v76
	v_mov_b32_e32 v92, v77
	v_pk_add_f32 v[76:77], v[78:79], v[98:99]
	v_pk_add_f32 v[78:79], v[78:79], v[98:99] neg_lo:[0,1] neg_hi:[0,1]
	s_nop 0
	v_pk_mul_f32 v[94:95], v[78:79], v[46:47] op_sel_hi:[1,0] neg_lo:[0,1] neg_hi:[0,1]
	s_nop 0
	v_pk_fma_f32 v[78:79], v[78:79], v[30:31], v[94:95] op_sel:[1,0,0] op_sel_hi:[0,0,1] neg_lo:[1,1,0] neg_hi:[0,1,0]
	s_waitcnt lgkmcnt(2)
	v_pk_add_f32 v[94:95], v[80:81], v[100:101]
	v_pk_add_f32 v[80:81], v[80:81], v[100:101] neg_lo:[0,1] neg_hi:[0,1]
	s_nop 0
	v_pk_mul_f32 v[96:97], v[80:81], v[36:37] op_sel_hi:[1,0] neg_lo:[0,1] neg_hi:[0,1]
	s_nop 0
	v_pk_fma_f32 v[80:81], v[80:81], v[32:33], v[96:97] op_sel:[1,0,0] op_sel_hi:[0,0,1] neg_lo:[1,1,0] neg_hi:[0,1,0]
	v_pk_add_f32 v[96:97], v[82:83], v[102:103]
	v_pk_add_f32 v[82:83], v[82:83], v[102:103] neg_lo:[0,1] neg_hi:[0,1]
	s_nop 0
	v_pk_mul_f32 v[98:99], v[82:83], v[38:39] op_sel_hi:[1,0] neg_lo:[0,1] neg_hi:[0,1]
	s_nop 0
	v_pk_fma_f32 v[82:83], v[82:83], v[34:35], v[98:99] op_sel:[1,0,0] op_sel_hi:[0,0,1] neg_lo:[1,1,0] neg_hi:[0,1,0]
	s_waitcnt lgkmcnt(1)
	v_pk_add_f32 v[98:99], v[84:85], v[104:105]
	v_pk_add_f32 v[84:85], v[84:85], v[104:105] neg_lo:[0,1] neg_hi:[0,1]
	s_nop 0
	v_pk_mul_f32 v[100:101], v[84:85], v[10:11] op_sel:[1,0] op_sel_hi:[0,0] neg_lo:[1,1] neg_hi:[0,1]
	s_nop 0
	v_pk_fma_f32 v[84:85], v[84:85], v[10:11], v[100:101] op_sel_hi:[1,0,1] neg_lo:[0,1,0] neg_hi:[0,1,0]
	v_pk_add_f32 v[100:101], v[86:87], v[106:107]
	v_pk_add_f32 v[86:87], v[86:87], v[106:107] neg_lo:[0,1] neg_hi:[0,1]
	s_nop 0
	v_pk_mul_f32 v[38:39], v[86:87], v[38:39] op_sel:[1,0] op_sel_hi:[0,0] neg_lo:[1,1] neg_hi:[0,1]
	s_nop 0
	v_pk_fma_f32 v[86:87], v[86:87], v[34:35], v[38:39] op_sel_hi:[1,0,1] neg_lo:[0,1,0] neg_hi:[0,1,0]
	s_waitcnt lgkmcnt(0)
	v_pk_add_f32 v[38:39], v[88:89], v[108:109] neg_lo:[0,1] neg_hi:[0,1]
	v_pk_add_f32 v[34:35], v[88:89], v[108:109]
	v_pk_mul_f32 v[88:89], v[38:39], v[36:37] op_sel:[1,0] op_sel_hi:[0,0] neg_lo:[1,1] neg_hi:[0,1]
	s_nop 0
	v_pk_fma_f32 v[88:89], v[38:39], v[32:33], v[88:89] op_sel_hi:[1,0,1] neg_lo:[0,1,0] neg_hi:[0,1,0]
	v_pk_add_f32 v[38:39], v[90:91], v[110:111]
	v_pk_add_f32 v[90:91], v[90:91], v[110:111] neg_lo:[0,1] neg_hi:[0,1]
	s_nop 0
	v_pk_mul_f32 v[46:47], v[90:91], v[46:47] op_sel:[1,0] op_sel_hi:[0,0] neg_lo:[1,1] neg_hi:[0,1]
	s_nop 0
	v_pk_fma_f32 v[90:91], v[90:91], v[30:31], v[46:47] op_sel_hi:[1,0,1] neg_lo:[0,1,0] neg_hi:[0,1,0]
	v_pk_add_f32 v[46:47], v[18:19], v[76:77]
	v_pk_add_f32 v[18:19], v[18:19], v[76:77] neg_lo:[0,1] neg_hi:[0,1]
	v_pk_add_f32 v[30:31], v[112:113], v[50:51]
	v_pk_mul_f32 v[76:77], v[18:19], v[36:37] op_sel:[1,0] op_sel_hi:[0,0] neg_lo:[1,1] neg_hi:[0,1]
	v_pk_add_f32 v[50:51], v[112:113], v[50:51] neg_lo:[0,1] neg_hi:[0,1]
	v_pk_fma_f32 v[76:77], v[18:19], v[32:33], v[76:77] op_sel_hi:[1,0,1]
	v_pk_add_f32 v[18:19], v[20:21], v[94:95]
	v_pk_add_f32 v[20:21], v[20:21], v[94:95] neg_lo:[0,1] neg_hi:[0,1]
	s_nop 0
	v_pk_mul_f32 v[94:95], v[20:21], v[10:11] op_sel:[1,0] op_sel_hi:[0,0] neg_lo:[1,1] neg_hi:[0,1]
	s_nop 0
	v_pk_fma_f32 v[20:21], v[20:21], v[10:11], v[94:95] op_sel_hi:[1,0,1]
	v_pk_add_f32 v[94:95], v[22:23], v[96:97]
	v_pk_add_f32 v[22:23], v[22:23], v[96:97] neg_lo:[0,1] neg_hi:[0,1]
	s_nop 0
	v_pk_mul_f32 v[96:97], v[22:23], v[36:37] op_sel_hi:[1,0]
	v_xor_b32_e32 v102, 0x80000000, v23
	v_mov_b32_e32 v103, v22
	v_pk_add_f32 v[22:23], v[24:25], v[98:99]
	v_pk_add_f32 v[24:25], v[24:25], v[98:99] neg_lo:[0,1] neg_hi:[0,1]
	v_pk_fma_f32 v[96:97], v[102:103], v[32:33], v[96:97] op_sel_hi:[1,0,1] neg_lo:[0,1,0] neg_hi:[0,1,0]
	v_xor_b32_e32 v99, 0x80000000, v24
	v_mov_b32_e32 v98, v25
	v_pk_add_f32 v[24:25], v[26:27], v[100:101]
	v_pk_add_f32 v[26:27], v[26:27], v[100:101] neg_lo:[0,1] neg_hi:[0,1]
	s_nop 0
	v_pk_mul_f32 v[100:101], v[26:27], v[36:37] op_sel_hi:[1,0] neg_lo:[0,1] neg_hi:[0,1]
	v_xor_b32_e32 v102, 0x80000000, v27
	v_mov_b32_e32 v103, v26
	v_pk_add_f32 v[26:27], v[28:29], v[34:35]
	v_pk_add_f32 v[28:29], v[28:29], v[34:35] neg_lo:[0,1] neg_hi:[0,1]
	v_pk_fma_f32 v[100:101], v[102:103], v[32:33], v[100:101] op_sel_hi:[1,0,1] neg_lo:[0,1,0] neg_hi:[0,1,0]
	v_pk_mul_f32 v[34:35], v[28:29], v[10:11] op_sel:[1,0] op_sel_hi:[0,0] neg_lo:[1,1] neg_hi:[0,1]
	v_pk_add_f32 v[102:103], v[30:31], v[22:23] neg_lo:[0,1] neg_hi:[0,1]
	v_pk_fma_f32 v[28:29], v[28:29], v[10:11], v[34:35] op_sel_hi:[1,0,1] neg_lo:[0,1,0] neg_hi:[0,1,0]
	v_pk_add_f32 v[34:35], v[42:43], v[38:39]
	v_pk_add_f32 v[38:39], v[42:43], v[38:39] neg_lo:[0,1] neg_hi:[0,1]
	s_nop 0
	v_pk_mul_f32 v[42:43], v[38:39], v[36:37] op_sel:[1,0] op_sel_hi:[0,0] neg_lo:[1,1] neg_hi:[0,1]
	s_nop 0
	v_pk_fma_f32 v[42:43], v[38:39], v[32:33], v[42:43] op_sel_hi:[1,0,1] neg_lo:[0,1,0] neg_hi:[0,1,0]
	v_pk_add_f32 v[38:39], v[30:31], v[22:23]
	v_pk_add_f32 v[22:23], v[46:47], v[24:25]
	v_pk_add_f32 v[24:25], v[46:47], v[24:25] neg_lo:[0,1] neg_hi:[0,1]
	s_nop 0
	v_pk_mul_f32 v[30:31], v[24:25], v[10:11] op_sel:[1,0] op_sel_hi:[0,0] neg_lo:[1,1] neg_hi:[0,1]
	s_nop 0
	v_pk_fma_f32 v[24:25], v[24:25], v[10:11], v[30:31] op_sel_hi:[1,0,1]
	v_pk_add_f32 v[30:31], v[18:19], v[26:27]
	v_pk_add_f32 v[18:19], v[18:19], v[26:27] neg_lo:[0,1] neg_hi:[0,1]
	s_nop 0
	v_xor_b32_e32 v27, 0x80000000, v18
	v_mov_b32_e32 v26, v19
	v_pk_add_f32 v[18:19], v[94:95], v[34:35]
	v_pk_add_f32 v[34:35], v[94:95], v[34:35] neg_lo:[0,1] neg_hi:[0,1]
	s_nop 0
	v_pk_mul_f32 v[46:47], v[34:35], v[10:11] op_sel:[1,0] op_sel_hi:[0,0] neg_lo:[1,1] neg_hi:[0,1]
	s_nop 0
	v_pk_fma_f32 v[34:35], v[34:35], v[10:11], v[46:47] op_sel_hi:[1,0,1] neg_lo:[0,1,0] neg_hi:[0,1,0]
	v_pk_add_f32 v[46:47], v[38:39], v[30:31]
	v_pk_add_f32 v[38:39], v[38:39], v[30:31] neg_lo:[0,1] neg_hi:[0,1]
	v_pk_add_f32 v[30:31], v[22:23], v[18:19]
	v_pk_add_f32 v[18:19], v[22:23], v[18:19] neg_lo:[0,1] neg_hi:[0,1]
	v_pk_add_f32 v[94:95], v[46:47], v[30:31]
	v_xor_b32_e32 v23, 0x80000000, v18
	v_mov_b32_e32 v22, v19
	v_pk_add_f32 v[18:19], v[102:103], v[26:27]
	v_pk_add_f32 v[102:103], v[102:103], v[26:27] neg_lo:[0,1] neg_hi:[0,1]
	v_pk_add_f32 v[26:27], v[24:25], v[34:35]
	v_pk_add_f32 v[24:25], v[24:25], v[34:35] neg_lo:[0,1] neg_hi:[0,1]
	v_pk_add_f32 v[30:31], v[46:47], v[30:31] neg_lo:[0,1] neg_hi:[0,1]
	v_xor_b32_e32 v35, 0x80000000, v24
	v_mov_b32_e32 v34, v25
	v_pk_add_f32 v[24:25], v[50:51], v[98:99]
	v_pk_add_f32 v[98:99], v[50:51], v[98:99] neg_lo:[0,1] neg_hi:[0,1]
	v_pk_add_f32 v[50:51], v[76:77], v[100:101] neg_lo:[0,1] neg_hi:[0,1]
	v_pk_add_f32 v[46:47], v[38:39], v[22:23]
	v_pk_add_f32 v[22:23], v[38:39], v[22:23] neg_lo:[0,1] neg_hi:[0,1]
	v_pk_add_f32 v[104:105], v[18:19], v[26:27]
	v_pk_add_f32 v[26:27], v[18:19], v[26:27] neg_lo:[0,1] neg_hi:[0,1]
	v_pk_add_f32 v[38:39], v[102:103], v[34:35]
	v_pk_add_f32 v[18:19], v[102:103], v[34:35] neg_lo:[0,1] neg_hi:[0,1]
	v_pk_add_f32 v[34:35], v[76:77], v[100:101]
	v_pk_mul_f32 v[76:77], v[10:11], v[50:51] op_sel:[0,1] op_sel_hi:[0,0] neg_lo:[1,1] neg_hi:[1,0]
	v_pk_fma_f32 v[76:77], v[10:11], v[50:51], v[76:77] op_sel_hi:[0,1,1]
	v_pk_add_f32 v[50:51], v[20:21], v[28:29]
	v_pk_add_f32 v[20:21], v[20:21], v[28:29] neg_lo:[0,1] neg_hi:[0,1]
	s_nop 0
	v_xor_b32_e32 v29, 0x80000000, v20
	v_mov_b32_e32 v28, v21
	v_pk_add_f32 v[20:21], v[96:97], v[42:43]
	v_pk_add_f32 v[42:43], v[96:97], v[42:43] neg_lo:[0,1] neg_hi:[0,1]
	s_nop 0
	v_pk_mul_f32 v[96:97], v[10:11], v[42:43] op_sel:[0,1] op_sel_hi:[0,0] neg_lo:[1,1] neg_hi:[1,0]
	v_pk_fma_f32 v[42:43], v[10:11], v[42:43], v[96:97] op_sel_hi:[0,1,1] neg_lo:[1,0,0] neg_hi:[1,0,0]
	v_pk_add_f32 v[96:97], v[24:25], v[50:51]
	v_pk_add_f32 v[24:25], v[24:25], v[50:51] neg_lo:[0,1] neg_hi:[0,1]
	v_pk_add_f32 v[50:51], v[34:35], v[20:21]
	v_pk_add_f32 v[20:21], v[34:35], v[20:21] neg_lo:[0,1] neg_hi:[0,1]
	v_pk_add_f32 v[102:103], v[96:97], v[50:51]
	v_xor_b32_e32 v101, 0x80000000, v20
	v_mov_b32_e32 v100, v21
	v_pk_add_f32 v[34:35], v[96:97], v[50:51] neg_lo:[0,1] neg_hi:[0,1]
	v_pk_add_f32 v[20:21], v[98:99], v[28:29]
	v_pk_add_f32 v[96:97], v[98:99], v[28:29] neg_lo:[0,1] neg_hi:[0,1]
	v_pk_add_f32 v[28:29], v[76:77], v[42:43]
	v_pk_add_f32 v[42:43], v[76:77], v[42:43] neg_lo:[0,1] neg_hi:[0,1]
	v_pk_add_f32 v[98:99], v[20:21], v[28:29]
	v_xor_b32_e32 v77, 0x80000000, v42
	v_mov_b32_e32 v76, v43
	v_pk_add_f32 v[28:29], v[20:21], v[28:29] neg_lo:[0,1] neg_hi:[0,1]
	v_pk_add_f32 v[42:43], v[96:97], v[76:77]
	v_pk_add_f32 v[20:21], v[96:97], v[76:77] neg_lo:[0,1] neg_hi:[0,1]
	v_pk_add_f32 v[76:77], v[40:41], v[92:93]
	v_pk_add_f32 v[92:93], v[40:41], v[92:93] neg_lo:[0,1] neg_hi:[0,1]
	v_pk_add_f32 v[40:41], v[44:45], v[78:79]
	v_pk_add_f32 v[44:45], v[44:45], v[78:79] neg_lo:[0,1] neg_hi:[0,1]
	v_pk_add_f32 v[50:51], v[24:25], v[100:101]
	v_pk_mul_f32 v[78:79], v[36:37], v[44:45] op_sel:[0,1] op_sel_hi:[0,0] neg_lo:[1,1] neg_hi:[1,0]
	v_pk_fma_f32 v[44:45], v[32:33], v[44:45], v[78:79] op_sel_hi:[0,1,1]
	v_pk_add_f32 v[78:79], v[48:49], v[80:81]
	v_pk_add_f32 v[48:49], v[48:49], v[80:81] neg_lo:[0,1] neg_hi:[0,1]
	v_pk_add_f32 v[24:25], v[24:25], v[100:101] neg_lo:[0,1] neg_hi:[0,1]
	v_pk_mul_f32 v[80:81], v[10:11], v[48:49] op_sel:[0,1] op_sel_hi:[0,0] neg_lo:[1,1] neg_hi:[1,0]
	v_pk_fma_f32 v[80:81], v[10:11], v[48:49], v[80:81] op_sel_hi:[0,1,1]
	v_pk_add_f32 v[48:49], v[52:53], v[82:83]
	v_pk_add_f32 v[52:53], v[52:53], v[82:83] neg_lo:[0,1] neg_hi:[0,1]
	s_nop 0
	v_pk_mul_f32 v[82:83], v[32:33], v[52:53] op_sel:[0,1] op_sel_hi:[0,0] neg_lo:[1,1] neg_hi:[1,0]
	v_pk_fma_f32 v[52:53], v[36:37], v[52:53], v[82:83] op_sel_hi:[0,1,1]
	v_pk_add_f32 v[82:83], v[54:55], v[84:85]
	v_pk_add_f32 v[54:55], v[54:55], v[84:85] neg_lo:[0,1] neg_hi:[0,1]
	s_nop 0
	v_xor_b32_e32 v85, 0x80000000, v54
	v_mov_b32_e32 v84, v55
	v_pk_add_f32 v[54:55], v[56:57], v[86:87]
	v_pk_add_f32 v[56:57], v[56:57], v[86:87] neg_lo:[0,1] neg_hi:[0,1]
	s_nop 0
	v_pk_mul_f32 v[86:87], v[32:33], v[56:57] op_sel:[0,1] op_sel_hi:[0,0] neg_lo:[1,1] neg_hi:[1,0]
	v_pk_fma_f32 v[56:57], v[36:37], v[56:57], v[86:87] op_sel_hi:[0,1,1] neg_lo:[1,0,0] neg_hi:[1,0,0]
	v_pk_add_f32 v[86:87], v[58:59], v[88:89]
	v_pk_add_f32 v[58:59], v[58:59], v[88:89] neg_lo:[0,1] neg_hi:[0,1]
	s_nop 0
	v_pk_mul_f32 v[88:89], v[10:11], v[58:59] op_sel:[0,1] op_sel_hi:[0,0] neg_lo:[1,1] neg_hi:[1,0]
	v_pk_fma_f32 v[58:59], v[10:11], v[58:59], v[88:89] op_sel_hi:[0,1,1] neg_lo:[1,0,0] neg_hi:[1,0,0]
	v_pk_add_f32 v[88:89], v[60:61], v[90:91]
	v_pk_add_f32 v[60:61], v[60:61], v[90:91] neg_lo:[0,1] neg_hi:[0,1]
	s_nop 0
	v_pk_mul_f32 v[36:37], v[36:37], v[60:61] op_sel:[0,1] op_sel_hi:[0,0] neg_lo:[1,1] neg_hi:[1,0]
	v_pk_fma_f32 v[36:37], v[32:33], v[60:61], v[36:37] op_sel_hi:[0,1,1] neg_lo:[1,0,0] neg_hi:[1,0,0]
	v_pk_add_f32 v[32:33], v[76:77], v[82:83]
	v_pk_add_f32 v[60:61], v[76:77], v[82:83] neg_lo:[0,1] neg_hi:[0,1]
	v_pk_add_f32 v[76:77], v[54:55], v[40:41]
	v_pk_add_f32 v[40:41], v[40:41], v[54:55] neg_lo:[0,1] neg_hi:[0,1]
	s_nop 0
	v_pk_mul_f32 v[54:55], v[10:11], v[40:41] op_sel:[0,1] op_sel_hi:[0,0] neg_lo:[1,1] neg_hi:[1,0]
	v_pk_fma_f32 v[54:55], v[10:11], v[40:41], v[54:55] op_sel_hi:[0,1,1]
	v_pk_add_f32 v[40:41], v[78:79], v[86:87]
	v_pk_add_f32 v[78:79], v[78:79], v[86:87] neg_lo:[0,1] neg_hi:[0,1]
	s_nop 0
	v_xor_b32_e32 v83, 0x80000000, v78
	v_mov_b32_e32 v82, v79
	v_pk_add_f32 v[78:79], v[48:49], v[88:89]
	v_pk_add_f32 v[48:49], v[48:49], v[88:89] neg_lo:[0,1] neg_hi:[0,1]
	v_pk_add_f32 v[88:89], v[76:77], v[78:79]
	v_pk_mul_f32 v[86:87], v[10:11], v[48:49] op_sel:[0,1] op_sel_hi:[0,0] neg_lo:[1,1] neg_hi:[1,0]
	v_pk_fma_f32 v[48:49], v[10:11], v[48:49], v[86:87] op_sel_hi:[0,1,1] neg_lo:[1,0,0] neg_hi:[1,0,0]
	v_pk_add_f32 v[86:87], v[32:33], v[40:41]
	v_pk_add_f32 v[32:33], v[32:33], v[40:41] neg_lo:[0,1] neg_hi:[0,1]
	v_pk_add_f32 v[40:41], v[76:77], v[78:79] neg_lo:[0,1] neg_hi:[0,1]
	v_pk_add_f32 v[78:79], v[86:87], v[88:89] neg_lo:[0,1] neg_hi:[0,1]
	v_pk_add_f32 v[90:91], v[32:33], v[40:41] op_sel:[0,1] op_sel_hi:[1,0] neg_hi:[0,1]
	v_pk_add_f32 v[40:41], v[32:33], v[40:41] op_sel:[0,1] op_sel_hi:[1,0] neg_lo:[0,1]
	v_pk_add_f32 v[76:77], v[54:55], v[48:49]
	v_pk_add_f32 v[48:49], v[54:55], v[48:49] neg_lo:[0,1] neg_hi:[0,1]
	v_pk_add_f32 v[32:33], v[60:61], v[82:83]
	v_pk_add_f32 v[60:61], v[60:61], v[82:83] neg_lo:[0,1] neg_hi:[0,1]
	v_xor_b32_e32 v55, 0x80000000, v48
	v_mov_b32_e32 v54, v49
	v_pk_add_f32 v[82:83], v[32:33], v[76:77]
	v_pk_add_f32 v[48:49], v[32:33], v[76:77] neg_lo:[0,1] neg_hi:[0,1]
	v_pk_add_f32 v[76:77], v[60:61], v[54:55]
	v_pk_add_f32 v[32:33], v[60:61], v[54:55] neg_lo:[0,1] neg_hi:[0,1]
	v_pk_add_f32 v[54:55], v[92:93], v[84:85]
	v_pk_add_f32 v[60:61], v[92:93], v[84:85] neg_lo:[0,1] neg_hi:[0,1]
	v_pk_add_f32 v[84:85], v[56:57], v[44:45]
	v_pk_add_f32 v[44:45], v[44:45], v[56:57] neg_lo:[0,1] neg_hi:[0,1]
	v_pk_add_f32 v[86:87], v[86:87], v[88:89]
	v_pk_mul_f32 v[56:57], v[10:11], v[44:45] op_sel:[0,1] op_sel_hi:[0,0] neg_lo:[1,1] neg_hi:[1,0]
	v_pk_fma_f32 v[56:57], v[10:11], v[44:45], v[56:57] op_sel_hi:[0,1,1]
	v_pk_add_f32 v[44:45], v[80:81], v[58:59]
	v_pk_add_f32 v[58:59], v[80:81], v[58:59] neg_lo:[0,1] neg_hi:[0,1]
	s_nop 0
	v_xor_b32_e32 v81, 0x80000000, v58
	v_mov_b32_e32 v80, v59
	v_pk_add_f32 v[58:59], v[52:53], v[36:37]
	v_pk_add_f32 v[36:37], v[52:53], v[36:37] neg_lo:[0,1] neg_hi:[0,1]
	s_nop 0
	v_pk_mul_f32 v[52:53], v[10:11], v[36:37] op_sel:[0,1] op_sel_hi:[0,0] neg_lo:[1,1] neg_hi:[1,0]
	v_pk_fma_f32 v[36:37], v[10:11], v[36:37], v[52:53] op_sel_hi:[0,1,1] neg_lo:[1,0,0] neg_hi:[1,0,0]
	v_pk_add_f32 v[52:53], v[54:55], v[44:45]
	v_pk_add_f32 v[44:45], v[54:55], v[44:45] neg_lo:[0,1] neg_hi:[0,1]
	v_pk_add_f32 v[54:55], v[84:85], v[58:59]
	v_pk_add_f32 v[58:59], v[84:85], v[58:59] neg_lo:[0,1] neg_hi:[0,1]
	s_nop 0
	v_xor_b32_e32 v85, 0x80000000, v58
	v_mov_b32_e32 v84, v59
	v_pk_add_f32 v[58:59], v[52:53], v[54:55]
	v_pk_add_f32 v[52:53], v[52:53], v[54:55] neg_lo:[0,1] neg_hi:[0,1]
	v_pk_add_f32 v[54:55], v[44:45], v[84:85]
	v_pk_add_f32 v[44:45], v[44:45], v[84:85] neg_lo:[0,1] neg_hi:[0,1]
	v_pk_add_f32 v[84:85], v[60:61], v[80:81]
	v_pk_add_f32 v[60:61], v[60:61], v[80:81] neg_lo:[0,1] neg_hi:[0,1]
	v_pk_add_f32 v[80:81], v[56:57], v[36:37]
	v_pk_add_f32 v[36:37], v[56:57], v[36:37] neg_lo:[0,1] neg_hi:[0,1]
	v_pk_add_f32 v[92:93], v[84:85], v[80:81]
	v_pk_add_f32 v[80:81], v[84:85], v[80:81] neg_lo:[0,1] neg_hi:[0,1]
	v_pk_add_f32 v[84:85], v[60:61], v[36:37] op_sel:[0,1] op_sel_hi:[1,0] neg_hi:[0,1]
	v_pk_add_f32 v[36:37], v[60:61], v[36:37] op_sel:[0,1] op_sel_hi:[1,0] neg_lo:[0,1]
	v_pk_fma_f32 v[60:61], v[16:17], s[90:91], v[16:17] op_sel:[1,0,0] op_sel_hi:[0,1,1]
	v_pk_mul_f32 v[56:57], v[94:95], s[14:15] op_sel:[1,0] neg_lo:[1,0]
	v_pk_mul_f32 v[88:89], v[60:61], v[86:87] op_sel:[1,1] op_sel_hi:[0,1] neg_lo:[0,1]
	v_pk_fma_f32 v[56:57], v[94:95], s[94:95], v[56:57] op_sel_hi:[0,1,1]
	v_pk_fma_f32 v[86:87], v[60:61], v[86:87], v[88:89] op_sel_hi:[1,0,1]
	ds_write2_b64 v75, v[56:57], v[86:87] offset1:16
	v_pk_mul_f32 v[56:57], v[16:17], v[60:61] op_sel:[1,1] op_sel_hi:[0,1] neg_lo:[0,1]
	v_pk_fma_f32 v[56:57], v[16:17], v[60:61], v[56:57] op_sel_hi:[1,0,1]
	s_nop 0
	v_pk_mul_f32 v[60:61], v[56:57], v[102:103] op_sel:[1,1] op_sel_hi:[0,1] neg_lo:[0,1]
	v_pk_mul_f32 v[86:87], v[16:17], v[56:57] op_sel:[1,1] op_sel_hi:[0,1] neg_lo:[0,1]
	v_pk_fma_f32 v[60:61], v[56:57], v[102:103], v[60:61] op_sel_hi:[1,0,1]
	v_pk_fma_f32 v[56:57], v[16:17], v[56:57], v[86:87] op_sel_hi:[1,0,1]
	s_nop 0
	v_pk_mul_f32 v[86:87], v[56:57], v[58:59] op_sel:[1,1] op_sel_hi:[0,1] neg_lo:[0,1]
	v_pk_fma_f32 v[58:59], v[56:57], v[58:59], v[86:87] op_sel_hi:[1,0,1]
	ds_write2_b64 v74, v[60:61], v[58:59] offset0:32 offset1:48
	v_pk_mul_f32 v[58:59], v[16:17], v[56:57] op_sel:[1,1] op_sel_hi:[0,1] neg_lo:[0,1]
	v_pk_fma_f32 v[56:57], v[16:17], v[56:57], v[58:59] op_sel_hi:[1,0,1]
	s_nop 0
	v_pk_mul_f32 v[58:59], v[56:57], v[104:105] op_sel:[1,1] op_sel_hi:[0,1] neg_lo:[0,1]
	v_pk_mul_f32 v[60:61], v[16:17], v[56:57] op_sel:[1,1] op_sel_hi:[0,1] neg_lo:[0,1]
	v_pk_fma_f32 v[58:59], v[56:57], v[104:105], v[58:59] op_sel_hi:[1,0,1]
	v_pk_fma_f32 v[56:57], v[16:17], v[56:57], v[60:61] op_sel_hi:[1,0,1]
	s_nop 0
	v_pk_mul_f32 v[60:61], v[56:57], v[82:83] op_sel:[1,1] op_sel_hi:[0,1] neg_lo:[0,1]
	v_pk_fma_f32 v[60:61], v[56:57], v[82:83], v[60:61] op_sel_hi:[1,0,1]
	ds_write2_b64 v73, v[58:59], v[60:61] offset0:64 offset1:80
	v_pk_mul_f32 v[58:59], v[16:17], v[56:57] op_sel:[1,1] op_sel_hi:[0,1] neg_lo:[0,1]
	v_pk_fma_f32 v[56:57], v[16:17], v[56:57], v[58:59] op_sel_hi:[1,0,1]
	s_nop 0
	v_pk_mul_f32 v[58:59], v[56:57], v[98:99] op_sel:[1,1] op_sel_hi:[0,1] neg_lo:[0,1]
	v_pk_mul_f32 v[60:61], v[16:17], v[56:57] op_sel:[1,1] op_sel_hi:[0,1] neg_lo:[0,1]
	v_pk_fma_f32 v[58:59], v[56:57], v[98:99], v[58:59] op_sel_hi:[1,0,1]
	v_pk_fma_f32 v[56:57], v[16:17], v[56:57], v[60:61] op_sel_hi:[1,0,1]
	s_nop 0
	v_pk_mul_f32 v[60:61], v[56:57], v[92:93] op_sel:[1,1] op_sel_hi:[0,1] neg_lo:[0,1]
	v_pk_fma_f32 v[60:61], v[56:57], v[92:93], v[60:61] op_sel_hi:[1,0,1]
	ds_write2_b64 v72, v[58:59], v[60:61] offset0:96 offset1:112
	v_pk_mul_f32 v[58:59], v[16:17], v[56:57] op_sel:[1,1] op_sel_hi:[0,1] neg_lo:[0,1]
	v_pk_fma_f32 v[56:57], v[16:17], v[56:57], v[58:59] op_sel_hi:[1,0,1]
	s_nop 0
	v_pk_mul_f32 v[58:59], v[56:57], v[46:47] op_sel:[1,1] op_sel_hi:[0,1] neg_lo:[0,1]
	v_pk_fma_f32 v[46:47], v[56:57], v[46:47], v[58:59] op_sel_hi:[1,0,1]
	v_pk_mul_f32 v[58:59], v[16:17], v[56:57] op_sel:[1,1] op_sel_hi:[0,1] neg_lo:[0,1]
	v_pk_fma_f32 v[56:57], v[16:17], v[56:57], v[58:59] op_sel_hi:[1,0,1]
	s_nop 0
	v_pk_mul_f32 v[58:59], v[56:57], v[90:91] op_sel:[1,1] op_sel_hi:[0,1] neg_lo:[0,1]
	v_pk_fma_f32 v[58:59], v[56:57], v[90:91], v[58:59] op_sel_hi:[1,0,1]
	ds_write2_b64 v71, v[46:47], v[58:59] offset0:128 offset1:144
	v_pk_mul_f32 v[46:47], v[16:17], v[56:57] op_sel:[1,1] op_sel_hi:[0,1] neg_lo:[0,1]
	v_pk_fma_f32 v[46:47], v[16:17], v[56:57], v[46:47] op_sel_hi:[1,0,1]
	s_nop 0
	v_pk_mul_f32 v[56:57], v[46:47], v[50:51] op_sel:[1,1] op_sel_hi:[0,1] neg_lo:[0,1]
	v_pk_fma_f32 v[50:51], v[46:47], v[50:51], v[56:57] op_sel_hi:[1,0,1]
	v_pk_mul_f32 v[56:57], v[16:17], v[46:47] op_sel:[1,1] op_sel_hi:[0,1] neg_lo:[0,1]
	v_pk_fma_f32 v[46:47], v[16:17], v[46:47], v[56:57] op_sel_hi:[1,0,1]
	s_nop 0
	v_pk_mul_f32 v[56:57], v[46:47], v[54:55] op_sel:[1,1] op_sel_hi:[0,1] neg_lo:[0,1]
	v_pk_fma_f32 v[54:55], v[46:47], v[54:55], v[56:57] op_sel_hi:[1,0,1]
	ds_write2_b64 v70, v[50:51], v[54:55] offset0:160 offset1:176
	v_pk_mul_f32 v[50:51], v[16:17], v[46:47] op_sel:[1,1] op_sel_hi:[0,1] neg_lo:[0,1]
	v_pk_fma_f32 v[46:47], v[16:17], v[46:47], v[50:51] op_sel_hi:[1,0,1]
	s_nop 0
	v_pk_mul_f32 v[50:51], v[38:39], v[46:47] op_sel:[1,1] op_sel_hi:[1,0] neg_lo:[1,0]
	s_nop 0
	v_pk_fma_f32 v[38:39], v[38:39], v[46:47], v[50:51] op_sel_hi:[0,1,1]
	v_pk_mul_f32 v[50:51], v[16:17], v[46:47] op_sel:[1,1] op_sel_hi:[0,1] neg_lo:[0,1]
	v_pk_fma_f32 v[46:47], v[16:17], v[46:47], v[50:51] op_sel_hi:[1,0,1]
	s_nop 0
	v_pk_mul_f32 v[50:51], v[46:47], v[76:77] op_sel:[1,1] op_sel_hi:[0,1] neg_lo:[0,1]
	v_pk_fma_f32 v[50:51], v[46:47], v[76:77], v[50:51] op_sel_hi:[1,0,1]
	ds_write2_b64 v69, v[38:39], v[50:51] offset0:192 offset1:208
	v_pk_mul_f32 v[38:39], v[16:17], v[46:47] op_sel:[1,1] op_sel_hi:[0,1] neg_lo:[0,1]
	v_pk_fma_f32 v[38:39], v[16:17], v[46:47], v[38:39] op_sel_hi:[1,0,1]
	s_nop 0
	v_pk_mul_f32 v[46:47], v[42:43], v[38:39] op_sel:[1,1] op_sel_hi:[1,0] neg_lo:[1,0]
	s_nop 0
	v_pk_fma_f32 v[42:43], v[42:43], v[38:39], v[46:47] op_sel_hi:[0,1,1]
	v_pk_mul_f32 v[46:47], v[16:17], v[38:39] op_sel:[1,1] op_sel_hi:[0,1] neg_lo:[0,1]
	v_pk_fma_f32 v[38:39], v[16:17], v[38:39], v[46:47] op_sel_hi:[1,0,1]
	s_nop 0
	v_pk_mul_f32 v[46:47], v[38:39], v[84:85] op_sel:[1,1] op_sel_hi:[0,1] neg_lo:[0,1]
	v_pk_fma_f32 v[46:47], v[38:39], v[84:85], v[46:47] op_sel_hi:[1,0,1]
	ds_write2_b64 v68, v[42:43], v[46:47] offset0:224 offset1:240
	v_pk_mul_f32 v[42:43], v[16:17], v[38:39] op_sel:[1,1] op_sel_hi:[0,1] neg_lo:[0,1]
	v_pk_fma_f32 v[38:39], v[16:17], v[38:39], v[42:43] op_sel_hi:[1,0,1]
	s_nop 0
	v_pk_mul_f32 v[42:43], v[30:31], v[38:39] op_sel:[1,1] op_sel_hi:[1,0] neg_lo:[1,0]
	s_nop 0
	v_pk_fma_f32 v[30:31], v[30:31], v[38:39], v[42:43] op_sel_hi:[0,1,1]
	v_pk_mul_f32 v[42:43], v[16:17], v[38:39] op_sel:[1,1] op_sel_hi:[0,1] neg_lo:[0,1]
	v_pk_fma_f32 v[38:39], v[16:17], v[38:39], v[42:43] op_sel_hi:[1,0,1]
	s_nop 0
	v_pk_mul_f32 v[42:43], v[78:79], v[38:39] op_sel:[1,1] op_sel_hi:[1,0] neg_lo:[1,0]
	s_nop 0
	v_pk_fma_f32 v[42:43], v[78:79], v[38:39], v[42:43] op_sel_hi:[0,1,1]
	ds_write2_b64 v67, v[30:31], v[42:43] offset1:16
	v_pk_mul_f32 v[30:31], v[16:17], v[38:39] op_sel:[1,1] op_sel_hi:[0,1] neg_lo:[0,1]
	v_pk_fma_f32 v[30:31], v[16:17], v[38:39], v[30:31] op_sel_hi:[1,0,1]
	s_nop 0
	v_pk_mul_f32 v[38:39], v[34:35], v[30:31] op_sel:[1,1] op_sel_hi:[1,0] neg_lo:[1,0]
	s_nop 0
	v_pk_fma_f32 v[34:35], v[34:35], v[30:31], v[38:39] op_sel_hi:[0,1,1]
	v_pk_mul_f32 v[38:39], v[16:17], v[30:31] op_sel:[1,1] op_sel_hi:[0,1] neg_lo:[0,1]
	v_pk_fma_f32 v[30:31], v[16:17], v[30:31], v[38:39] op_sel_hi:[1,0,1]
	s_nop 0
	v_pk_mul_f32 v[38:39], v[52:53], v[30:31] op_sel:[1,1] op_sel_hi:[1,0] neg_lo:[1,0]
	s_nop 0
	v_pk_fma_f32 v[38:39], v[52:53], v[30:31], v[38:39] op_sel_hi:[0,1,1]
	ds_write2_b64 v66, v[34:35], v[38:39] offset0:32 offset1:48
	v_pk_mul_f32 v[34:35], v[16:17], v[30:31] op_sel:[1,1] op_sel_hi:[0,1] neg_lo:[0,1]
	v_pk_fma_f32 v[30:31], v[16:17], v[30:31], v[34:35] op_sel_hi:[1,0,1]
	s_nop 0
	v_pk_mul_f32 v[34:35], v[26:27], v[30:31] op_sel:[1,1] op_sel_hi:[1,0] neg_lo:[1,0]
	s_nop 0
	v_pk_fma_f32 v[26:27], v[26:27], v[30:31], v[34:35] op_sel_hi:[0,1,1]
	v_pk_mul_f32 v[34:35], v[16:17], v[30:31] op_sel:[1,1] op_sel_hi:[0,1] neg_lo:[0,1]
	v_pk_fma_f32 v[30:31], v[16:17], v[30:31], v[34:35] op_sel_hi:[1,0,1]
	s_nop 0
	v_pk_mul_f32 v[34:35], v[48:49], v[30:31] op_sel:[1,1] op_sel_hi:[1,0] neg_lo:[1,0]
	s_nop 0
	v_pk_fma_f32 v[34:35], v[48:49], v[30:31], v[34:35] op_sel_hi:[0,1,1]
	ds_write2_b64 v65, v[26:27], v[34:35] offset0:64 offset1:80
	v_pk_mul_f32 v[26:27], v[16:17], v[30:31] op_sel:[1,1] op_sel_hi:[0,1] neg_lo:[0,1]
	v_pk_fma_f32 v[26:27], v[16:17], v[30:31], v[26:27] op_sel_hi:[1,0,1]
	s_nop 0
	v_pk_mul_f32 v[30:31], v[28:29], v[26:27] op_sel:[1,1] op_sel_hi:[1,0] neg_lo:[1,0]
	s_nop 0
	v_pk_fma_f32 v[28:29], v[28:29], v[26:27], v[30:31] op_sel_hi:[0,1,1]
	v_pk_mul_f32 v[30:31], v[16:17], v[26:27] op_sel:[1,1] op_sel_hi:[0,1] neg_lo:[0,1]
	v_pk_fma_f32 v[26:27], v[16:17], v[26:27], v[30:31] op_sel_hi:[1,0,1]
	s_nop 0
	v_pk_mul_f32 v[30:31], v[80:81], v[26:27] op_sel:[1,1] op_sel_hi:[1,0] neg_lo:[1,0]
	s_nop 0
	v_pk_fma_f32 v[30:31], v[80:81], v[26:27], v[30:31] op_sel_hi:[0,1,1]
	ds_write2_b64 v64, v[28:29], v[30:31] offset0:96 offset1:112
	v_pk_mul_f32 v[28:29], v[16:17], v[26:27] op_sel:[1,1] op_sel_hi:[0,1] neg_lo:[0,1]
	v_pk_fma_f32 v[26:27], v[16:17], v[26:27], v[28:29] op_sel_hi:[1,0,1]
	s_nop 0
	v_pk_mul_f32 v[28:29], v[22:23], v[26:27] op_sel:[1,1] op_sel_hi:[1,0] neg_lo:[1,0]
	s_nop 0
	v_pk_fma_f32 v[22:23], v[22:23], v[26:27], v[28:29] op_sel_hi:[0,1,1]
	v_pk_mul_f32 v[28:29], v[16:17], v[26:27] op_sel:[1,1] op_sel_hi:[0,1] neg_lo:[0,1]
	v_pk_fma_f32 v[26:27], v[16:17], v[26:27], v[28:29] op_sel_hi:[1,0,1]
	s_nop 0
	v_pk_mul_f32 v[28:29], v[40:41], v[26:27] op_sel:[1,1] op_sel_hi:[1,0] neg_lo:[1,0]
	s_nop 0
	v_pk_fma_f32 v[28:29], v[40:41], v[26:27], v[28:29] op_sel_hi:[0,1,1]
	ds_write2_b64 v63, v[22:23], v[28:29] offset0:128 offset1:144
	v_pk_mul_f32 v[22:23], v[16:17], v[26:27] op_sel:[1,1] op_sel_hi:[0,1] neg_lo:[0,1]
	v_pk_fma_f32 v[22:23], v[16:17], v[26:27], v[22:23] op_sel_hi:[1,0,1]
	s_nop 0
	v_pk_mul_f32 v[26:27], v[24:25], v[22:23] op_sel:[1,1] op_sel_hi:[1,0] neg_lo:[1,0]
	s_nop 0
	v_pk_fma_f32 v[24:25], v[24:25], v[22:23], v[26:27] op_sel_hi:[0,1,1]
	v_pk_mul_f32 v[26:27], v[16:17], v[22:23] op_sel:[1,1] op_sel_hi:[0,1] neg_lo:[0,1]
	v_pk_fma_f32 v[22:23], v[16:17], v[22:23], v[26:27] op_sel_hi:[1,0,1]
	s_nop 0
	v_pk_mul_f32 v[26:27], v[44:45], v[22:23] op_sel:[1,1] op_sel_hi:[1,0] neg_lo:[1,0]
	s_nop 0
	v_pk_fma_f32 v[26:27], v[44:45], v[22:23], v[26:27] op_sel_hi:[0,1,1]
	ds_write2_b64 v62, v[24:25], v[26:27] offset0:160 offset1:176
	v_pk_mul_f32 v[24:25], v[16:17], v[22:23] op_sel:[1,1] op_sel_hi:[0,1] neg_lo:[0,1]
	v_pk_fma_f32 v[22:23], v[16:17], v[22:23], v[24:25] op_sel_hi:[1,0,1]
	s_nop 0
	v_pk_mul_f32 v[24:25], v[18:19], v[22:23] op_sel:[1,1] op_sel_hi:[1,0] neg_lo:[1,0]
	s_nop 0
	v_pk_fma_f32 v[18:19], v[18:19], v[22:23], v[24:25] op_sel_hi:[0,1,1]
	v_pk_mul_f32 v[24:25], v[16:17], v[22:23] op_sel:[1,1] op_sel_hi:[0,1] neg_lo:[0,1]
	v_pk_fma_f32 v[22:23], v[16:17], v[22:23], v[24:25] op_sel_hi:[1,0,1]
	s_nop 0
	v_pk_mul_f32 v[24:25], v[32:33], v[22:23] op_sel:[1,1] op_sel_hi:[1,0] neg_lo:[1,0]
	s_nop 0
	v_pk_fma_f32 v[24:25], v[32:33], v[22:23], v[24:25] op_sel_hi:[0,1,1]
	ds_write2_b64 v15, v[18:19], v[24:25] offset0:192 offset1:208
	v_pk_mul_f32 v[18:19], v[16:17], v[22:23] op_sel:[1,1] op_sel_hi:[0,1] neg_lo:[0,1]
	v_pk_fma_f32 v[18:19], v[16:17], v[22:23], v[18:19] op_sel_hi:[1,0,1]
	s_nop 0
	v_pk_mul_f32 v[22:23], v[20:21], v[18:19] op_sel:[1,1] op_sel_hi:[1,0] neg_lo:[1,0]
	s_nop 0
	v_pk_fma_f32 v[20:21], v[20:21], v[18:19], v[22:23] op_sel_hi:[0,1,1]
	v_pk_mul_f32 v[22:23], v[16:17], v[18:19] op_sel:[1,1] op_sel_hi:[0,1] neg_lo:[0,1]
	v_pk_fma_f32 v[16:17], v[16:17], v[18:19], v[22:23] op_sel_hi:[1,0,1]
	s_nop 0
	v_pk_mul_f32 v[18:19], v[36:37], v[16:17] op_sel:[1,1] op_sel_hi:[1,0] neg_lo:[1,0]
	s_nop 0
	v_pk_fma_f32 v[16:17], v[36:37], v[16:17], v[18:19] op_sel_hi:[0,1,1]
	ds_write2_b64 v13, v[20:21], v[16:17] offset0:224 offset1:240
	v_mov_b32_e32 v16, v182
	v_mov_b32_e32 v10, v176
	v_mov_b32_e32 v17, v175
	s_waitcnt lgkmcnt(0)
	s_barrier
	v_lshlrev_b32_e32 v190, 3, v16
	v_add_u32_e32 v190, 0x1000, v190
	global_load_dwordx2 v[202:203], v190, s[46:47] offset:-4096
	global_load_dwordx2 v[204:205], v190, s[46:47]
	v_add_u32_e32 v190, 0x2000, v190
	global_load_dwordx2 v[206:207], v190, s[46:47] offset:-4096
	global_load_dwordx2 v[208:209], v190, s[46:47]
	v_add_u32_e32 v190, 0x2000, v190
	global_load_dwordx2 v[210:211], v190, s[46:47] offset:-4096
	global_load_dwordx2 v[212:213], v190, s[46:47]
	v_add_u32_e32 v190, 0x2000, v190
	global_load_dwordx2 v[214:215], v190, s[46:47] offset:-4096
	global_load_dwordx2 v[216:217], v190, s[46:47]
	v_add_u32_e32 v190, 0x2000, v190
	global_load_dwordx2 v[218:219], v190, s[46:47] offset:-4096
	global_load_dwordx2 v[220:221], v190, s[46:47]
	v_add_u32_e32 v190, 0x2000, v190
	global_load_dwordx2 v[222:223], v190, s[46:47] offset:-4096
	global_load_dwordx2 v[224:225], v190, s[46:47]
	v_add_u32_e32 v190, 0x2000, v190
	global_load_dwordx2 v[226:227], v190, s[46:47] offset:-4096
	global_load_dwordx2 v[228:229], v190, s[46:47]
	v_add_u32_e32 v190, 0x2000, v190
	global_load_dwordx2 v[230:231], v190, s[46:47] offset:-4096
	global_load_dwordx2 v[232:233], v190, s[46:47]
	v_mov_b32_e32 v50, v165
	v_lshlrev_b32_e32 v13, 3, v17
	v_lshlrev_b32_e32 v48, 3, v10
	v_add3_u32 v10, 0, v13, v48
	v_xor_b32_e32 v13, 1, v17
	v_xor_b32_e32 v34, 8, v17
	v_xor_b32_e32 v36, 9, v17
	v_lshlrev_b32_e32 v13, 3, v13
	v_xor_b32_e32 v15, 2, v17
	v_xor_b32_e32 v24, 3, v17
	v_xor_b32_e32 v26, 4, v17
	v_xor_b32_e32 v28, 5, v17
	v_xor_b32_e32 v30, 6, v17
	v_xor_b32_e32 v32, 7, v17
	v_lshlrev_b32_e32 v34, 3, v34
	v_lshlrev_b32_e32 v36, 3, v36
	v_xor_b32_e32 v38, 10, v17
	v_xor_b32_e32 v40, 11, v17
	v_xor_b32_e32 v42, 12, v17
	v_xor_b32_e32 v44, 13, v17
	v_xor_b32_e32 v46, 14, v17
	v_xor_b32_e32 v17, 15, v17
	v_add3_u32 v13, 0, v13, v48
	v_lshlrev_b32_e32 v15, 3, v15
	v_lshlrev_b32_e32 v24, 3, v24
	v_lshlrev_b32_e32 v26, 3, v26
	v_lshlrev_b32_e32 v28, 3, v28
	v_lshlrev_b32_e32 v30, 3, v30
	v_lshlrev_b32_e32 v32, 3, v32
	v_add3_u32 v57, 0, v34, v48
	v_add3_u32 v58, 0, v36, v48
	v_lshlrev_b32_e32 v38, 3, v38
	v_lshlrev_b32_e32 v40, 3, v40
	v_lshlrev_b32_e32 v42, 3, v42
	v_lshlrev_b32_e32 v44, 3, v44
	v_lshlrev_b32_e32 v46, 3, v46
	v_lshlrev_b32_e32 v17, 3, v17
	ds_read_b64 v[18:19], v10
	ds_read_b64 v[20:21], v13
	v_add3_u32 v15, 0, v15, v48
	v_add3_u32 v52, 0, v24, v48
	v_add3_u32 v53, 0, v26, v48
	v_add3_u32 v54, 0, v28, v48
	v_add3_u32 v55, 0, v30, v48
	v_add3_u32 v56, 0, v32, v48
	ds_read_b64 v[34:35], v57
	ds_read_b64 v[36:37], v58
	v_add3_u32 v59, 0, v38, v48
	v_add3_u32 v60, 0, v40, v48
	v_add3_u32 v61, 0, v42, v48
	v_add3_u32 v62, 0, v44, v48
	v_add3_u32 v63, 0, v46, v48
	v_add3_u32 v64, 0, v17, v48
	ds_read_b64 v[22:23], v15
	ds_read_b64 v[24:25], v52
	ds_read_b64 v[26:27], v53
	ds_read_b64 v[28:29], v54
	ds_read_b64 v[30:31], v55
	ds_read_b64 v[32:33], v56
	ds_read_b64 v[38:39], v59
	ds_read_b64 v[40:41], v60
	ds_read_b64 v[42:43], v61
	ds_read_b64 v[44:45], v62
	ds_read_b64 v[46:47], v63
	ds_read_b64 v[48:49], v64
	s_waitcnt lgkmcnt(13)
	v_pk_add_f32 v[70:71], v[18:19], v[34:35]
	v_pk_add_f32 v[18:19], v[18:19], v[34:35] neg_lo:[0,1] neg_hi:[0,1]
	s_waitcnt lgkmcnt(12)
	v_pk_add_f32 v[34:35], v[20:21], v[36:37]
	v_pk_add_f32 v[20:21], v[20:21], v[36:37] neg_lo:[0,1] neg_hi:[0,1]
	v_mov_b32_e32 v66, v167
	v_mov_b32_e32 v68, v169
	s_nop 0
	v_pk_mul_f32 v[36:37], v[20:21], v[68:69] op_sel:[1,0] op_sel_hi:[0,0] neg_lo:[1,1] neg_hi:[0,1]
	v_pk_fma_f32 v[20:21], v[20:21], v[50:51], v[36:37] op_sel_hi:[1,0,1]
	s_waitcnt lgkmcnt(5)
	v_pk_add_f32 v[36:37], v[22:23], v[38:39]
	v_pk_add_f32 v[22:23], v[22:23], v[38:39] neg_lo:[0,1] neg_hi:[0,1]
	s_nop 0
	v_pk_mul_f32 v[38:39], v[22:23], v[66:67] op_sel:[1,0] op_sel_hi:[0,0] neg_lo:[1,1] neg_hi:[0,1]
	v_pk_fma_f32 v[22:23], v[22:23], v[66:67], v[38:39] op_sel_hi:[1,0,1]
	s_waitcnt lgkmcnt(4)
	v_pk_add_f32 v[38:39], v[24:25], v[40:41]
	v_pk_add_f32 v[24:25], v[24:25], v[40:41] neg_lo:[0,1] neg_hi:[0,1]
	s_nop 0
	v_pk_mul_f32 v[40:41], v[24:25], v[68:69] op_sel_hi:[1,0]
	s_nop 0
	v_pk_fma_f32 v[24:25], v[24:25], v[50:51], v[40:41] op_sel:[1,0,0] op_sel_hi:[0,0,1] neg_lo:[1,1,0] neg_hi:[0,1,0]
	s_waitcnt lgkmcnt(3)
	v_pk_add_f32 v[40:41], v[26:27], v[42:43]
	v_pk_add_f32 v[26:27], v[26:27], v[42:43] neg_lo:[0,1] neg_hi:[0,1]
	v_xor_b32_e32 v73, 0x80000000, v26
	v_mov_b32_e32 v72, v27
	s_waitcnt lgkmcnt(2)
	v_pk_add_f32 v[26:27], v[28:29], v[44:45]
	v_pk_add_f32 v[28:29], v[28:29], v[44:45] neg_lo:[0,1] neg_hi:[0,1]
	s_nop 0
	v_pk_mul_f32 v[42:43], v[28:29], v[68:69] op_sel_hi:[1,0] neg_lo:[0,1] neg_hi:[0,1]
	s_nop 0
	v_pk_fma_f32 v[28:29], v[28:29], v[50:51], v[42:43] op_sel:[1,0,0] op_sel_hi:[0,0,1] neg_lo:[1,1,0] neg_hi:[0,1,0]
	s_waitcnt lgkmcnt(1)
	v_pk_add_f32 v[42:43], v[30:31], v[46:47]
	v_pk_add_f32 v[30:31], v[30:31], v[46:47] neg_lo:[0,1] neg_hi:[0,1]
	s_nop 0
	v_pk_mul_f32 v[44:45], v[30:31], v[66:67] op_sel:[1,0] op_sel_hi:[0,0] neg_lo:[1,1] neg_hi:[0,1]
	s_nop 0
	v_pk_fma_f32 v[30:31], v[30:31], v[66:67], v[44:45] op_sel_hi:[1,0,1] neg_lo:[0,1,0] neg_hi:[0,1,0]
	s_waitcnt lgkmcnt(0)
	v_pk_add_f32 v[44:45], v[32:33], v[48:49]
	v_pk_add_f32 v[32:33], v[32:33], v[48:49] neg_lo:[0,1] neg_hi:[0,1]
	v_pk_add_f32 v[48:49], v[34:35], v[26:27]
	v_pk_add_f32 v[26:27], v[34:35], v[26:27] neg_lo:[0,1] neg_hi:[0,1]
	s_nop 0
	v_pk_mul_f32 v[34:35], v[26:27], v[66:67] op_sel:[1,0] op_sel_hi:[0,0] neg_lo:[1,1] neg_hi:[0,1]
	v_pk_fma_f32 v[26:27], v[26:27], v[66:67], v[34:35] op_sel_hi:[1,0,1]
	v_pk_add_f32 v[34:35], v[36:37], v[42:43]
	v_pk_add_f32 v[36:37], v[36:37], v[42:43] neg_lo:[0,1] neg_hi:[0,1]
	v_pk_mul_f32 v[46:47], v[32:33], v[68:69] op_sel:[1,0] op_sel_hi:[0,0] neg_lo:[1,1] neg_hi:[0,1]
	v_xor_b32_e32 v43, 0x80000000, v36
	v_mov_b32_e32 v42, v37
	v_pk_add_f32 v[36:37], v[38:39], v[44:45]
	v_pk_add_f32 v[38:39], v[38:39], v[44:45] neg_lo:[0,1] neg_hi:[0,1]
	v_pk_fma_f32 v[46:47], v[32:33], v[50:51], v[46:47] op_sel_hi:[1,0,1] neg_lo:[0,1,0] neg_hi:[0,1,0]
	v_pk_add_f32 v[32:33], v[70:71], v[40:41]
	v_pk_mul_f32 v[44:45], v[38:39], v[66:67] op_sel:[1,0] op_sel_hi:[0,0] neg_lo:[1,1] neg_hi:[0,1]
	v_pk_add_f32 v[40:41], v[70:71], v[40:41] neg_lo:[0,1] neg_hi:[0,1]
	v_pk_fma_f32 v[38:39], v[38:39], v[66:67], v[44:45] op_sel_hi:[1,0,1] neg_lo:[0,1,0] neg_hi:[0,1,0]
	v_pk_add_f32 v[44:45], v[32:33], v[34:35]
	v_pk_add_f32 v[32:33], v[32:33], v[34:35] neg_lo:[0,1] neg_hi:[0,1]
	v_pk_add_f32 v[34:35], v[48:49], v[36:37]
	v_pk_add_f32 v[36:37], v[48:49], v[36:37] neg_lo:[0,1] neg_hi:[0,1]
	v_pk_add_f32 v[50:51], v[44:45], v[34:35]
	v_xor_b32_e32 v49, 0x80000000, v36
	v_mov_b32_e32 v48, v37
	v_pk_add_f32 v[36:37], v[44:45], v[34:35] neg_lo:[0,1] neg_hi:[0,1]
	v_pk_add_f32 v[68:69], v[32:33], v[48:49]
	v_pk_add_f32 v[44:45], v[32:33], v[48:49] neg_lo:[0,1] neg_hi:[0,1]
	v_pk_add_f32 v[32:33], v[40:41], v[42:43]
	v_pk_add_f32 v[34:35], v[40:41], v[42:43] neg_lo:[0,1] neg_hi:[0,1]
	v_pk_add_f32 v[40:41], v[26:27], v[38:39]
	v_pk_add_f32 v[26:27], v[26:27], v[38:39] neg_lo:[0,1] neg_hi:[0,1]
	v_pk_add_f32 v[42:43], v[32:33], v[40:41] neg_lo:[0,1] neg_hi:[0,1]
	v_xor_b32_e32 v39, 0x80000000, v26
	v_mov_b32_e32 v38, v27
	v_pk_add_f32 v[26:27], v[32:33], v[40:41]
	v_pk_add_f32 v[40:41], v[20:21], v[28:29]
	v_pk_add_f32 v[20:21], v[20:21], v[28:29] neg_lo:[0,1] neg_hi:[0,1]
	v_pk_add_f32 v[32:33], v[34:35], v[38:39]
	v_pk_mul_f32 v[28:29], v[66:67], v[20:21] op_sel:[0,1] op_sel_hi:[0,0] neg_lo:[1,1] neg_hi:[1,0]
	v_pk_fma_f32 v[20:21], v[66:67], v[20:21], v[28:29] op_sel_hi:[0,1,1]
	v_pk_add_f32 v[28:29], v[22:23], v[30:31]
	v_pk_add_f32 v[22:23], v[22:23], v[30:31] neg_lo:[0,1] neg_hi:[0,1]
	v_pk_add_f32 v[38:39], v[34:35], v[38:39] neg_lo:[0,1] neg_hi:[0,1]
	v_xor_b32_e32 v31, 0x80000000, v22
	v_mov_b32_e32 v30, v23
	v_pk_add_f32 v[22:23], v[24:25], v[46:47]
	v_pk_add_f32 v[24:25], v[24:25], v[46:47] neg_lo:[0,1] neg_hi:[0,1]
	v_pk_add_f32 v[34:35], v[18:19], v[72:73]
	v_pk_mul_f32 v[46:47], v[66:67], v[24:25] op_sel:[0,1] op_sel_hi:[0,0] neg_lo:[1,1] neg_hi:[1,0]
	v_pk_fma_f32 v[24:25], v[66:67], v[24:25], v[46:47] op_sel_hi:[0,1,1] neg_lo:[1,0,0] neg_hi:[1,0,0]
	v_pk_add_f32 v[46:47], v[34:35], v[28:29]
	v_pk_add_f32 v[28:29], v[34:35], v[28:29] neg_lo:[0,1] neg_hi:[0,1]
	v_pk_add_f32 v[34:35], v[40:41], v[22:23]
	v_pk_add_f32 v[22:23], v[40:41], v[22:23] neg_lo:[0,1] neg_hi:[0,1]
	v_pk_add_f32 v[18:19], v[18:19], v[72:73] neg_lo:[0,1] neg_hi:[0,1]
	v_pk_add_f32 v[66:67], v[28:29], v[22:23] op_sel:[0,1] op_sel_hi:[1,0] neg_hi:[0,1]
	v_pk_add_f32 v[48:49], v[28:29], v[22:23] op_sel:[0,1] op_sel_hi:[1,0] neg_lo:[0,1]
	v_pk_add_f32 v[28:29], v[18:19], v[30:31]
	v_pk_add_f32 v[18:19], v[18:19], v[30:31] neg_lo:[0,1] neg_hi:[0,1]
	v_pk_add_f32 v[30:31], v[20:21], v[24:25]
	v_pk_add_f32 v[20:21], v[20:21], v[24:25] neg_lo:[0,1] neg_hi:[0,1]
	v_pk_add_f32 v[22:23], v[46:47], v[34:35]
	v_xor_b32_e32 v25, 0x80000000, v20
	v_mov_b32_e32 v24, v21
	s_waitcnt vmcnt(0)
	v_pk_add_f32 v[40:41], v[46:47], v[34:35] neg_lo:[0,1] neg_hi:[0,1]
	v_pk_add_f32 v[34:35], v[18:19], v[24:25]
	v_pk_add_f32 v[18:19], v[18:19], v[24:25] neg_lo:[0,1] neg_hi:[0,1]
	v_pk_add_f32 v[70:71], v[28:29], v[30:31]
	v_pk_add_f32 v[46:47], v[28:29], v[30:31] neg_lo:[0,1] neg_hi:[0,1]
	s_nop 0
	v_pk_mul_f32 v[24:25], v[50:51], v[202:203] op_sel:[1,1] op_sel_hi:[1,0] neg_lo:[1,0]
	s_nop 0
	v_pk_fma_f32 v[20:21], v[50:51], v[202:203], v[24:25] op_sel_hi:[0,1,1]
	s_nop 0
	v_pk_mul_f32 v[28:29], v[204:205], v[22:23] op_sel:[1,1] op_sel_hi:[0,1] neg_lo:[0,1]
	v_pk_fma_f32 v[22:23], v[204:205], v[22:23], v[28:29] op_sel_hi:[1,0,1]
	s_nop 0
	v_pk_mul_f32 v[28:29], v[26:27], v[206:207] op_sel:[1,1] op_sel_hi:[1,0] neg_lo:[1,0]
	s_nop 0
	v_pk_fma_f32 v[24:25], v[26:27], v[206:207], v[28:29] op_sel_hi:[0,1,1]
	s_nop 0
	v_pk_mul_f32 v[28:29], v[208:209], v[70:71] op_sel:[1,1] op_sel_hi:[0,1] neg_lo:[0,1]
	v_pk_fma_f32 v[26:27], v[208:209], v[70:71], v[28:29] op_sel_hi:[1,0,1]
	s_nop 0
	v_pk_mul_f32 v[30:31], v[68:69], v[210:211] op_sel:[1,1] op_sel_hi:[1,0] neg_lo:[1,0]
	s_nop 0
	v_pk_fma_f32 v[28:29], v[68:69], v[210:211], v[30:31] op_sel_hi:[0,1,1]
	v_mov_b32_e32 v68, v169
	s_nop 0
	v_pk_mul_f32 v[50:51], v[212:213], v[66:67] op_sel:[1,1] op_sel_hi:[0,1] neg_lo:[0,1]
	v_pk_fma_f32 v[30:31], v[212:213], v[66:67], v[50:51] op_sel_hi:[1,0,1]
	s_nop 0
	v_pk_mul_f32 v[66:67], v[32:33], v[214:215] op_sel:[1,1] op_sel_hi:[1,0] neg_lo:[1,0]
	s_nop 0
	v_pk_fma_f32 v[32:33], v[32:33], v[214:215], v[66:67] op_sel_hi:[0,1,1]
	s_nop 0
	v_pk_mul_f32 v[66:67], v[216:217], v[34:35] op_sel:[1,1] op_sel_hi:[0,1] neg_lo:[0,1]
	v_pk_fma_f32 v[34:35], v[216:217], v[34:35], v[66:67] op_sel_hi:[1,0,1]
	s_nop 0
	v_pk_mul_f32 v[66:67], v[36:37], v[218:219] op_sel:[1,1] op_sel_hi:[1,0] neg_lo:[1,0]
	s_nop 0
	v_pk_fma_f32 v[36:37], v[36:37], v[218:219], v[66:67] op_sel_hi:[0,1,1]
	v_pk_add_f32 v[70:71], v[20:21], v[36:37]
	v_pk_add_f32 v[20:21], v[20:21], v[36:37] neg_lo:[0,1] neg_hi:[0,1]
	s_nop 0
	v_pk_mul_f32 v[66:67], v[40:41], v[220:221] op_sel:[1,1] op_sel_hi:[1,0] neg_lo:[1,0]
	s_nop 0
	v_pk_fma_f32 v[40:41], v[40:41], v[220:221], v[66:67] op_sel_hi:[0,1,1]
	v_pk_add_f32 v[36:37], v[22:23], v[40:41]
	v_pk_add_f32 v[22:23], v[22:23], v[40:41] neg_lo:[0,1] neg_hi:[0,1]
	s_nop 0
	v_pk_mul_f32 v[66:67], v[42:43], v[222:223] op_sel:[1,1] op_sel_hi:[1,0] neg_lo:[1,0]
	s_nop 0
	v_pk_fma_f32 v[42:43], v[42:43], v[222:223], v[66:67] op_sel_hi:[0,1,1]
	s_nop 0
	v_pk_mul_f32 v[66:67], v[46:47], v[224:225] op_sel:[1,1] op_sel_hi:[1,0] neg_lo:[1,0]
	s_nop 0
	v_pk_fma_f32 v[46:47], v[46:47], v[224:225], v[66:67] op_sel_hi:[0,1,1]
	s_nop 0
	v_pk_mul_f32 v[66:67], v[44:45], v[226:227] op_sel:[1,1] op_sel_hi:[1,0] neg_lo:[1,0]
	s_nop 0
	v_pk_fma_f32 v[44:45], v[44:45], v[226:227], v[66:67] op_sel_hi:[0,1,1]
	s_nop 0
	v_pk_mul_f32 v[66:67], v[48:49], v[228:229] op_sel:[1,1] op_sel_hi:[1,0] neg_lo:[1,0]
	s_nop 0
	v_pk_fma_f32 v[48:49], v[48:49], v[228:229], v[66:67] op_sel_hi:[0,1,1]
	s_nop 0
	v_pk_mul_f32 v[66:67], v[38:39], v[230:231] op_sel:[1,1] op_sel_hi:[1,0] neg_lo:[1,0]
	s_nop 0
	v_pk_fma_f32 v[38:39], v[38:39], v[230:231], v[66:67] op_sel_hi:[0,1,1]
	v_mov_b32_e32 v50, v232
	v_mov_b32_e32 v51, v233
	v_lshlrev_b32_e32 v190, 3, v16
	v_add_u32_e32 v190, 0x11000, v190
	global_load_dwordx2 v[202:203], v190, s[46:47] offset:-4096
	global_load_dwordx2 v[204:205], v190, s[46:47]
	v_add_u32_e32 v190, 0x2000, v190
	global_load_dwordx2 v[206:207], v190, s[46:47] offset:-4096
	global_load_dwordx2 v[208:209], v190, s[46:47]
	v_add_u32_e32 v190, 0x2000, v190
	global_load_dwordx2 v[210:211], v190, s[46:47] offset:-4096
	global_load_dwordx2 v[212:213], v190, s[46:47]
	v_add_u32_e32 v190, 0x2000, v190
	global_load_dwordx2 v[214:215], v190, s[46:47] offset:-4096
	global_load_dwordx2 v[216:217], v190, s[46:47]
	v_add_u32_e32 v190, 0x2000, v190
	global_load_dwordx2 v[218:219], v190, s[46:47] offset:-4096
	global_load_dwordx2 v[220:221], v190, s[46:47]
	v_add_u32_e32 v190, 0x2000, v190
	global_load_dwordx2 v[222:223], v190, s[46:47] offset:-4096
	global_load_dwordx2 v[224:225], v190, s[46:47]
	v_add_u32_e32 v190, 0x2000, v190
	global_load_dwordx2 v[226:227], v190, s[46:47] offset:-4096
	global_load_dwordx2 v[228:229], v190, s[46:47]
	v_add_u32_e32 v190, 0x2000, v190
	global_load_dwordx2 v[230:231], v190, s[46:47] offset:-4096
	global_load_dwordx2 v[232:233], v190, s[46:47]
	s_nop 0
	v_pk_mul_f32 v[66:67], v[18:19], v[50:51] op_sel:[1,1] op_sel_hi:[1,0] neg_lo:[1,0]
	s_nop 0
	v_pk_fma_f32 v[18:19], v[18:19], v[50:51], v[66:67] op_sel_hi:[0,1,1]
	v_mov_b32_e32 v50, v165
	v_mov_b32_e32 v66, v167
	s_nop 0
	v_pk_mul_f32 v[40:41], v[22:23], v[68:69] op_sel:[1,0] op_sel_hi:[0,0] neg_lo:[1,0]
	v_pk_fma_f32 v[22:23], v[22:23], v[50:51], v[40:41] op_sel_hi:[1,0,1]
	v_pk_add_f32 v[40:41], v[24:25], v[42:43]
	v_pk_add_f32 v[24:25], v[24:25], v[42:43] neg_lo:[0,1] neg_hi:[0,1]
	s_nop 0
	v_pk_mul_f32 v[42:43], v[24:25], v[66:67] op_sel:[1,0] op_sel_hi:[0,0] neg_lo:[1,0]
	v_pk_fma_f32 v[24:25], v[24:25], v[66:67], v[42:43] op_sel_hi:[1,0,1]
	v_pk_add_f32 v[42:43], v[26:27], v[46:47]
	v_pk_add_f32 v[26:27], v[26:27], v[46:47] neg_lo:[0,1] neg_hi:[0,1]
	s_nop 0
	v_pk_mul_f32 v[46:47], v[26:27], v[68:69] op_sel_hi:[1,0]
	s_nop 0
	v_pk_fma_f32 v[26:27], v[26:27], v[50:51], v[46:47] op_sel:[1,0,0] op_sel_hi:[0,0,1] neg_lo:[1,0,0]
	v_pk_add_f32 v[46:47], v[28:29], v[44:45]
	v_pk_add_f32 v[28:29], v[28:29], v[44:45] neg_lo:[0,1] neg_hi:[0,1]
	v_mov_b32_e32 v17, v175
	v_xor_b32_e32 v44, 0x80000000, v29
	v_mov_b32_e32 v45, v28
	v_pk_add_f32 v[28:29], v[30:31], v[48:49]
	v_pk_add_f32 v[30:31], v[30:31], v[48:49] neg_lo:[0,1] neg_hi:[0,1]
	s_nop 0
	v_pk_mul_f32 v[48:49], v[30:31], v[68:69] op_sel_hi:[1,0] neg_lo:[0,1] neg_hi:[0,1]
	s_nop 0
	v_pk_fma_f32 v[30:31], v[30:31], v[50:51], v[48:49] op_sel:[1,0,0] op_sel_hi:[0,0,1] neg_lo:[1,0,0]
	v_pk_add_f32 v[48:49], v[32:33], v[38:39]
	v_pk_add_f32 v[32:33], v[32:33], v[38:39] neg_lo:[0,1] neg_hi:[0,1]
	s_nop 0
	v_pk_mul_f32 v[38:39], v[32:33], v[66:67] op_sel:[1,0] op_sel_hi:[0,0] neg_lo:[1,0]
	s_nop 0
	v_pk_fma_f32 v[32:33], v[32:33], v[66:67], v[38:39] op_sel_hi:[1,0,1] neg_lo:[0,1,0] neg_hi:[0,1,0]
	v_pk_add_f32 v[38:39], v[34:35], v[18:19]
	v_pk_add_f32 v[18:19], v[34:35], v[18:19] neg_lo:[0,1] neg_hi:[0,1]
	s_nop 0
	v_pk_mul_f32 v[34:35], v[18:19], v[68:69] op_sel:[1,0] op_sel_hi:[0,0] neg_lo:[1,0]
	v_mov_b32_e32 v68, v169
	v_pk_fma_f32 v[18:19], v[18:19], v[50:51], v[34:35] op_sel_hi:[1,0,1] neg_lo:[0,1,0] neg_hi:[0,1,0]
	v_pk_add_f32 v[50:51], v[36:37], v[28:29]
	v_pk_add_f32 v[28:29], v[36:37], v[28:29] neg_lo:[0,1] neg_hi:[0,1]
	v_pk_add_f32 v[34:35], v[70:71], v[46:47]
	v_pk_mul_f32 v[36:37], v[28:29], v[66:67] op_sel:[1,0] op_sel_hi:[0,0] neg_lo:[1,0]
	v_pk_add_f32 v[46:47], v[70:71], v[46:47] neg_lo:[0,1] neg_hi:[0,1]
	v_pk_fma_f32 v[28:29], v[28:29], v[66:67], v[36:37] op_sel_hi:[1,0,1]
	v_pk_add_f32 v[36:37], v[40:41], v[48:49]
	v_pk_add_f32 v[40:41], v[40:41], v[48:49] neg_lo:[0,1] neg_hi:[0,1]
	s_nop 0
	v_xor_b32_e32 v48, 0x80000000, v41
	v_mov_b32_e32 v49, v40
	v_pk_add_f32 v[40:41], v[42:43], v[38:39]
	v_pk_add_f32 v[38:39], v[42:43], v[38:39] neg_lo:[0,1] neg_hi:[0,1]
	s_nop 0
	v_pk_mul_f32 v[42:43], v[66:67], v[38:39] op_sel:[0,1] op_sel_hi:[0,0] neg_lo:[0,1]
	v_pk_fma_f32 v[38:39], v[38:39], v[66:67], v[42:43] op_sel_hi:[1,0,1] neg_lo:[0,1,0] neg_hi:[0,1,0]
	v_pk_add_f32 v[42:43], v[34:35], v[36:37]
	v_pk_add_f32 v[34:35], v[34:35], v[36:37] neg_lo:[0,1] neg_hi:[0,1]
	v_pk_add_f32 v[36:37], v[50:51], v[40:41]
	v_pk_add_f32 v[40:41], v[50:51], v[40:41] neg_lo:[0,1] neg_hi:[0,1]
	s_nop 0
	v_xor_b32_e32 v50, 0x80000000, v41
	v_mov_b32_e32 v51, v40
	v_pk_add_f32 v[40:41], v[42:43], v[36:37]
	v_pk_add_f32 v[36:37], v[42:43], v[36:37] neg_lo:[0,1] neg_hi:[0,1]
	v_pk_add_f32 v[42:43], v[34:35], v[50:51]
	v_pk_add_f32 v[34:35], v[34:35], v[50:51] neg_lo:[0,1] neg_hi:[0,1]
	v_pk_add_f32 v[50:51], v[46:47], v[48:49]
	v_pk_add_f32 v[46:47], v[46:47], v[48:49] neg_lo:[0,1] neg_hi:[0,1]
	v_pk_add_f32 v[48:49], v[28:29], v[38:39]
	v_pk_add_f32 v[28:29], v[28:29], v[38:39] neg_lo:[0,1] neg_hi:[0,1]
	s_nop 0
	v_xor_b32_e32 v38, 0x80000000, v29
	v_mov_b32_e32 v39, v28
	v_pk_add_f32 v[28:29], v[50:51], v[48:49]
	v_pk_add_f32 v[48:49], v[50:51], v[48:49] neg_lo:[0,1] neg_hi:[0,1]
	v_pk_add_f32 v[50:51], v[46:47], v[38:39]
	v_pk_add_f32 v[38:39], v[46:47], v[38:39] neg_lo:[0,1] neg_hi:[0,1]
	v_pk_add_f32 v[46:47], v[20:21], v[44:45]
	v_pk_add_f32 v[20:21], v[20:21], v[44:45] neg_lo:[0,1] neg_hi:[0,1]
	v_pk_add_f32 v[44:45], v[22:23], v[30:31]
	v_pk_add_f32 v[22:23], v[22:23], v[30:31] neg_lo:[0,1] neg_hi:[0,1]
	s_nop 0
	v_pk_mul_f32 v[30:31], v[66:67], v[22:23] op_sel:[0,1] op_sel_hi:[0,0] neg_lo:[0,1]
	v_pk_fma_f32 v[22:23], v[66:67], v[22:23], v[30:31] op_sel_hi:[0,1,1]
	v_pk_add_f32 v[30:31], v[24:25], v[32:33]
	v_pk_add_f32 v[24:25], v[24:25], v[32:33] neg_lo:[0,1] neg_hi:[0,1]
	s_nop 0
	v_xor_b32_e32 v32, 0x80000000, v25
	v_mov_b32_e32 v33, v24
	v_pk_add_f32 v[24:25], v[26:27], v[18:19]
	v_pk_add_f32 v[18:19], v[26:27], v[18:19] neg_lo:[0,1] neg_hi:[0,1]
	s_nop 0
	v_pk_mul_f32 v[26:27], v[66:67], v[18:19] op_sel:[0,1] op_sel_hi:[0,0] neg_lo:[0,1]
	v_pk_fma_f32 v[18:19], v[66:67], v[18:19], v[26:27] op_sel_hi:[0,1,1] neg_lo:[1,0,0] neg_hi:[1,0,0]
	v_pk_add_f32 v[26:27], v[46:47], v[30:31]
	v_pk_add_f32 v[30:31], v[46:47], v[30:31] neg_lo:[0,1] neg_hi:[0,1]
	v_pk_add_f32 v[46:47], v[44:45], v[24:25]
	v_pk_add_f32 v[24:25], v[44:45], v[24:25] neg_lo:[0,1] neg_hi:[0,1]
	v_mov_b32_e32 v66, v167
	v_xor_b32_e32 v44, 0x80000000, v25
	v_mov_b32_e32 v45, v24
	v_pk_add_f32 v[24:25], v[26:27], v[46:47]
	v_pk_add_f32 v[26:27], v[26:27], v[46:47] neg_lo:[0,1] neg_hi:[0,1]
	v_pk_add_f32 v[46:47], v[30:31], v[44:45]
	v_pk_add_f32 v[30:31], v[30:31], v[44:45] neg_lo:[0,1] neg_hi:[0,1]
	v_pk_add_f32 v[44:45], v[20:21], v[32:33]
	v_pk_add_f32 v[20:21], v[20:21], v[32:33] neg_lo:[0,1] neg_hi:[0,1]
	v_pk_add_f32 v[32:33], v[22:23], v[18:19]
	v_pk_add_f32 v[18:19], v[22:23], v[18:19] neg_lo:[0,1] neg_hi:[0,1]
	s_nop 0
	v_xor_b32_e32 v22, 0x80000000, v19
	v_mov_b32_e32 v23, v18
	v_pk_add_f32 v[18:19], v[44:45], v[32:33]
	v_pk_add_f32 v[32:33], v[44:45], v[32:33] neg_lo:[0,1] neg_hi:[0,1]
	v_pk_add_f32 v[44:45], v[20:21], v[22:23]
	v_pk_add_f32 v[20:21], v[20:21], v[22:23] neg_lo:[0,1] neg_hi:[0,1]
	ds_write_b64 v10, v[40:41]
	ds_write_b64 v13, v[24:25]
	ds_write_b64 v15, v[28:29]
	ds_write_b64 v52, v[18:19]
	ds_write_b64 v53, v[42:43]
	ds_write_b64 v54, v[46:47]
	ds_write_b64 v55, v[50:51]
	ds_write_b64 v56, v[44:45]
	ds_write_b64 v57, v[36:37]
	ds_write_b64 v58, v[26:27]
	ds_write_b64 v59, v[48:49]
	ds_write_b64 v60, v[32:33]
	ds_write_b64 v61, v[34:35]
	ds_write_b64 v62, v[30:31]
	ds_write_b64 v63, v[38:39]
	ds_write_b64 v64, v[20:21]
	v_mov_b32_e32 v10, v177
	v_mov_b32_e32 v64, v165
	v_lshlrev_b32_e32 v13, 3, v17
	v_lshlrev_b32_e32 v48, 3, v10
	v_add3_u32 v10, 0, v13, v48
	v_xor_b32_e32 v13, 1, v17
	v_xor_b32_e32 v34, 8, v17
	v_xor_b32_e32 v36, 9, v17
	v_lshlrev_b32_e32 v13, 3, v13
	v_xor_b32_e32 v15, 2, v17
	v_xor_b32_e32 v24, 3, v17
	v_xor_b32_e32 v26, 4, v17
	v_xor_b32_e32 v28, 5, v17
	v_xor_b32_e32 v30, 6, v17
	v_xor_b32_e32 v32, 7, v17
	v_lshlrev_b32_e32 v34, 3, v34
	v_lshlrev_b32_e32 v36, 3, v36
	v_xor_b32_e32 v38, 10, v17
	v_xor_b32_e32 v40, 11, v17
	v_xor_b32_e32 v42, 12, v17
	v_xor_b32_e32 v44, 13, v17
	v_xor_b32_e32 v46, 14, v17
	v_xor_b32_e32 v17, 15, v17
	v_add3_u32 v13, 0, v13, v48
	v_lshlrev_b32_e32 v15, 3, v15
	v_lshlrev_b32_e32 v24, 3, v24
	v_lshlrev_b32_e32 v26, 3, v26
	v_lshlrev_b32_e32 v28, 3, v28
	v_lshlrev_b32_e32 v30, 3, v30
	v_lshlrev_b32_e32 v32, 3, v32
	v_add3_u32 v55, 0, v34, v48
	v_add3_u32 v56, 0, v36, v48
	v_lshlrev_b32_e32 v38, 3, v38
	v_lshlrev_b32_e32 v40, 3, v40
	v_lshlrev_b32_e32 v42, 3, v42
	v_lshlrev_b32_e32 v44, 3, v44
	v_lshlrev_b32_e32 v46, 3, v46
	v_lshlrev_b32_e32 v17, 3, v17
	ds_read_b64 v[18:19], v10
	ds_read_b64 v[20:21], v13
	v_add3_u32 v15, 0, v15, v48
	v_add3_u32 v50, 0, v24, v48
	v_add3_u32 v51, 0, v26, v48
	v_add3_u32 v52, 0, v28, v48
	v_add3_u32 v53, 0, v30, v48
	v_add3_u32 v54, 0, v32, v48
	ds_read_b64 v[34:35], v55
	ds_read_b64 v[36:37], v56
	v_add3_u32 v57, 0, v38, v48
	v_add3_u32 v58, 0, v40, v48
	v_add3_u32 v59, 0, v42, v48
	v_add3_u32 v60, 0, v44, v48
	v_add3_u32 v61, 0, v46, v48
	v_add3_u32 v62, 0, v17, v48
	ds_read_b64 v[22:23], v15
	ds_read_b64 v[24:25], v50
	ds_read_b64 v[26:27], v51
	ds_read_b64 v[28:29], v52
	ds_read_b64 v[30:31], v53
	ds_read_b64 v[32:33], v54
	ds_read_b64 v[38:39], v57
	ds_read_b64 v[40:41], v58
	ds_read_b64 v[42:43], v59
	ds_read_b64 v[44:45], v60
	ds_read_b64 v[46:47], v61
	ds_read_b64 v[48:49], v62
	s_waitcnt lgkmcnt(13)
	v_pk_add_f32 v[70:71], v[18:19], v[34:35]
	v_pk_add_f32 v[18:19], v[18:19], v[34:35] neg_lo:[0,1] neg_hi:[0,1]
	s_waitcnt lgkmcnt(12)
	v_pk_add_f32 v[34:35], v[20:21], v[36:37]
	v_pk_add_f32 v[20:21], v[20:21], v[36:37] neg_lo:[0,1] neg_hi:[0,1]
	s_nop 0
	v_pk_mul_f32 v[36:37], v[20:21], v[68:69] op_sel:[1,0] op_sel_hi:[0,0] neg_lo:[1,1] neg_hi:[0,1]
	v_pk_fma_f32 v[20:21], v[20:21], v[64:65], v[36:37] op_sel_hi:[1,0,1]
	s_waitcnt lgkmcnt(5)
	v_pk_add_f32 v[36:37], v[22:23], v[38:39]
	v_pk_add_f32 v[22:23], v[22:23], v[38:39] neg_lo:[0,1] neg_hi:[0,1]
	s_nop 0
	v_pk_mul_f32 v[38:39], v[22:23], v[66:67] op_sel:[1,0] op_sel_hi:[0,0] neg_lo:[1,1] neg_hi:[0,1]
	v_pk_fma_f32 v[22:23], v[22:23], v[66:67], v[38:39] op_sel_hi:[1,0,1]
	s_waitcnt lgkmcnt(4)
	v_pk_add_f32 v[38:39], v[24:25], v[40:41]
	v_pk_add_f32 v[24:25], v[24:25], v[40:41] neg_lo:[0,1] neg_hi:[0,1]
	s_nop 0
	v_pk_mul_f32 v[40:41], v[24:25], v[68:69] op_sel_hi:[1,0]
	s_nop 0
	v_pk_fma_f32 v[24:25], v[24:25], v[64:65], v[40:41] op_sel:[1,0,0] op_sel_hi:[0,0,1] neg_lo:[1,1,0] neg_hi:[0,1,0]
	s_waitcnt lgkmcnt(3)
	v_pk_add_f32 v[40:41], v[26:27], v[42:43]
	v_pk_add_f32 v[26:27], v[26:27], v[42:43] neg_lo:[0,1] neg_hi:[0,1]
	s_nop 0
	v_xor_b32_e32 v73, 0x80000000, v26
	v_mov_b32_e32 v72, v27
	s_waitcnt lgkmcnt(2)
	v_pk_add_f32 v[26:27], v[28:29], v[44:45]
	v_pk_add_f32 v[28:29], v[28:29], v[44:45] neg_lo:[0,1] neg_hi:[0,1]
	s_nop 0
	v_pk_mul_f32 v[42:43], v[28:29], v[68:69] op_sel_hi:[1,0] neg_lo:[0,1] neg_hi:[0,1]
	s_nop 0
	v_pk_fma_f32 v[28:29], v[28:29], v[64:65], v[42:43] op_sel:[1,0,0] op_sel_hi:[0,0,1] neg_lo:[1,1,0] neg_hi:[0,1,0]
	s_waitcnt lgkmcnt(1)
	v_pk_add_f32 v[42:43], v[30:31], v[46:47]
	v_pk_add_f32 v[30:31], v[30:31], v[46:47] neg_lo:[0,1] neg_hi:[0,1]
	s_nop 0
	v_pk_mul_f32 v[44:45], v[30:31], v[66:67] op_sel:[1,0] op_sel_hi:[0,0] neg_lo:[1,1] neg_hi:[0,1]
	s_nop 0
	v_pk_fma_f32 v[30:31], v[30:31], v[66:67], v[44:45] op_sel_hi:[1,0,1] neg_lo:[0,1,0] neg_hi:[0,1,0]
	s_waitcnt lgkmcnt(0)
	v_pk_add_f32 v[44:45], v[32:33], v[48:49]
	v_pk_add_f32 v[32:33], v[32:33], v[48:49] neg_lo:[0,1] neg_hi:[0,1]
	v_pk_add_f32 v[48:49], v[34:35], v[26:27]
	v_pk_add_f32 v[26:27], v[34:35], v[26:27] neg_lo:[0,1] neg_hi:[0,1]
	s_nop 0
	v_pk_mul_f32 v[34:35], v[26:27], v[66:67] op_sel:[1,0] op_sel_hi:[0,0] neg_lo:[1,1] neg_hi:[0,1]
	v_pk_fma_f32 v[26:27], v[26:27], v[66:67], v[34:35] op_sel_hi:[1,0,1]
	v_pk_add_f32 v[34:35], v[36:37], v[42:43]
	v_pk_add_f32 v[36:37], v[36:37], v[42:43] neg_lo:[0,1] neg_hi:[0,1]
	v_pk_mul_f32 v[46:47], v[32:33], v[68:69] op_sel:[1,0] op_sel_hi:[0,0] neg_lo:[1,1] neg_hi:[0,1]
	v_xor_b32_e32 v43, 0x80000000, v36
	v_mov_b32_e32 v42, v37
	v_pk_add_f32 v[36:37], v[38:39], v[44:45]
	v_pk_add_f32 v[38:39], v[38:39], v[44:45] neg_lo:[0,1] neg_hi:[0,1]
	v_pk_fma_f32 v[46:47], v[32:33], v[64:65], v[46:47] op_sel_hi:[1,0,1] neg_lo:[0,1,0] neg_hi:[0,1,0]
	v_pk_add_f32 v[32:33], v[70:71], v[40:41]
	v_pk_mul_f32 v[44:45], v[38:39], v[66:67] op_sel:[1,0] op_sel_hi:[0,0] neg_lo:[1,1] neg_hi:[0,1]
	v_pk_add_f32 v[40:41], v[70:71], v[40:41] neg_lo:[0,1] neg_hi:[0,1]
	v_pk_fma_f32 v[38:39], v[38:39], v[66:67], v[44:45] op_sel_hi:[1,0,1] neg_lo:[0,1,0] neg_hi:[0,1,0]
	v_pk_add_f32 v[44:45], v[32:33], v[34:35]
	v_pk_add_f32 v[32:33], v[32:33], v[34:35] neg_lo:[0,1] neg_hi:[0,1]
	v_pk_add_f32 v[34:35], v[48:49], v[36:37]
	v_pk_add_f32 v[36:37], v[48:49], v[36:37] neg_lo:[0,1] neg_hi:[0,1]
	v_pk_add_f32 v[64:65], v[44:45], v[34:35]
	v_xor_b32_e32 v49, 0x80000000, v36
	v_mov_b32_e32 v48, v37
	v_pk_add_f32 v[36:37], v[44:45], v[34:35] neg_lo:[0,1] neg_hi:[0,1]
	v_pk_add_f32 v[68:69], v[32:33], v[48:49]
	v_pk_add_f32 v[44:45], v[32:33], v[48:49] neg_lo:[0,1] neg_hi:[0,1]
	v_pk_add_f32 v[32:33], v[40:41], v[42:43]
	v_pk_add_f32 v[34:35], v[40:41], v[42:43] neg_lo:[0,1] neg_hi:[0,1]
	v_pk_add_f32 v[40:41], v[26:27], v[38:39]
	v_pk_add_f32 v[26:27], v[26:27], v[38:39] neg_lo:[0,1] neg_hi:[0,1]
	v_pk_add_f32 v[42:43], v[32:33], v[40:41] neg_lo:[0,1] neg_hi:[0,1]
	v_xor_b32_e32 v39, 0x80000000, v26
	v_mov_b32_e32 v38, v27
	v_pk_add_f32 v[26:27], v[32:33], v[40:41]
	v_pk_add_f32 v[40:41], v[20:21], v[28:29]
	v_pk_add_f32 v[20:21], v[20:21], v[28:29] neg_lo:[0,1] neg_hi:[0,1]
	v_pk_add_f32 v[32:33], v[34:35], v[38:39]
	v_pk_mul_f32 v[28:29], v[66:67], v[20:21] op_sel:[0,1] op_sel_hi:[0,0] neg_lo:[1,1] neg_hi:[1,0]
	v_pk_fma_f32 v[20:21], v[66:67], v[20:21], v[28:29] op_sel_hi:[0,1,1]
	v_pk_add_f32 v[28:29], v[22:23], v[30:31]
	v_pk_add_f32 v[22:23], v[22:23], v[30:31] neg_lo:[0,1] neg_hi:[0,1]
	v_pk_add_f32 v[38:39], v[34:35], v[38:39] neg_lo:[0,1] neg_hi:[0,1]
	v_xor_b32_e32 v31, 0x80000000, v22
	v_mov_b32_e32 v30, v23
	v_pk_add_f32 v[22:23], v[24:25], v[46:47]
	v_pk_add_f32 v[24:25], v[24:25], v[46:47] neg_lo:[0,1] neg_hi:[0,1]
	v_pk_add_f32 v[34:35], v[18:19], v[72:73]
	v_pk_mul_f32 v[46:47], v[66:67], v[24:25] op_sel:[0,1] op_sel_hi:[0,0] neg_lo:[1,1] neg_hi:[1,0]
	v_pk_fma_f32 v[24:25], v[66:67], v[24:25], v[46:47] op_sel_hi:[0,1,1] neg_lo:[1,0,0] neg_hi:[1,0,0]
	v_pk_add_f32 v[46:47], v[34:35], v[28:29]
	v_pk_add_f32 v[28:29], v[34:35], v[28:29] neg_lo:[0,1] neg_hi:[0,1]
	v_pk_add_f32 v[34:35], v[40:41], v[22:23]
	v_pk_add_f32 v[22:23], v[40:41], v[22:23] neg_lo:[0,1] neg_hi:[0,1]
	v_pk_add_f32 v[18:19], v[18:19], v[72:73] neg_lo:[0,1] neg_hi:[0,1]
	v_pk_add_f32 v[66:67], v[28:29], v[22:23] op_sel:[0,1] op_sel_hi:[1,0] neg_hi:[0,1]
	v_pk_add_f32 v[48:49], v[28:29], v[22:23] op_sel:[0,1] op_sel_hi:[1,0] neg_lo:[0,1]
	v_pk_add_f32 v[28:29], v[18:19], v[30:31]
	v_pk_add_f32 v[18:19], v[18:19], v[30:31] neg_lo:[0,1] neg_hi:[0,1]
	v_pk_add_f32 v[30:31], v[20:21], v[24:25]
	v_pk_add_f32 v[20:21], v[20:21], v[24:25] neg_lo:[0,1] neg_hi:[0,1]
	v_pk_add_f32 v[22:23], v[46:47], v[34:35]
	v_xor_b32_e32 v25, 0x80000000, v20
	v_mov_b32_e32 v24, v21
	s_waitcnt vmcnt(0)
	v_pk_add_f32 v[40:41], v[46:47], v[34:35] neg_lo:[0,1] neg_hi:[0,1]
	v_pk_add_f32 v[34:35], v[18:19], v[24:25]
	v_pk_add_f32 v[18:19], v[18:19], v[24:25] neg_lo:[0,1] neg_hi:[0,1]
	v_pk_add_f32 v[70:71], v[28:29], v[30:31]
	v_pk_add_f32 v[46:47], v[28:29], v[30:31] neg_lo:[0,1] neg_hi:[0,1]
	s_nop 0
	v_pk_mul_f32 v[24:25], v[64:65], v[202:203] op_sel:[1,1] op_sel_hi:[1,0] neg_lo:[1,0]
	s_nop 0
	v_pk_fma_f32 v[20:21], v[64:65], v[202:203], v[24:25] op_sel_hi:[0,1,1]
	s_nop 0
	v_pk_mul_f32 v[28:29], v[204:205], v[22:23] op_sel:[1,1] op_sel_hi:[0,1] neg_lo:[0,1]
	v_pk_fma_f32 v[22:23], v[204:205], v[22:23], v[28:29] op_sel_hi:[1,0,1]
	s_nop 0
	v_pk_mul_f32 v[28:29], v[26:27], v[206:207] op_sel:[1,1] op_sel_hi:[1,0] neg_lo:[1,0]
	s_nop 0
	v_pk_fma_f32 v[24:25], v[26:27], v[206:207], v[28:29] op_sel_hi:[0,1,1]
	s_nop 0
	v_pk_mul_f32 v[28:29], v[208:209], v[70:71] op_sel:[1,1] op_sel_hi:[0,1] neg_lo:[0,1]
	v_pk_fma_f32 v[26:27], v[208:209], v[70:71], v[28:29] op_sel_hi:[1,0,1]
	s_nop 0
	v_pk_mul_f32 v[30:31], v[68:69], v[210:211] op_sel:[1,1] op_sel_hi:[1,0] neg_lo:[1,0]
	s_nop 0
	v_pk_fma_f32 v[28:29], v[68:69], v[210:211], v[30:31] op_sel_hi:[0,1,1]
	s_nop 0
	v_pk_mul_f32 v[64:65], v[212:213], v[66:67] op_sel:[1,1] op_sel_hi:[0,1] neg_lo:[0,1]
	v_pk_fma_f32 v[30:31], v[212:213], v[66:67], v[64:65] op_sel_hi:[1,0,1]
	s_nop 0
	v_pk_mul_f32 v[66:67], v[32:33], v[214:215] op_sel:[1,1] op_sel_hi:[1,0] neg_lo:[1,0]
	s_nop 0
	v_pk_fma_f32 v[32:33], v[32:33], v[214:215], v[66:67] op_sel_hi:[0,1,1]
	s_nop 0
	v_pk_mul_f32 v[66:67], v[216:217], v[34:35] op_sel:[1,1] op_sel_hi:[0,1] neg_lo:[0,1]
	v_pk_fma_f32 v[34:35], v[216:217], v[34:35], v[66:67] op_sel_hi:[1,0,1]
	s_nop 0
	v_pk_mul_f32 v[66:67], v[36:37], v[218:219] op_sel:[1,1] op_sel_hi:[1,0] neg_lo:[1,0]
	s_nop 0
	v_pk_fma_f32 v[36:37], v[36:37], v[218:219], v[66:67] op_sel_hi:[0,1,1]
	v_pk_add_f32 v[68:69], v[20:21], v[36:37]
	v_pk_add_f32 v[20:21], v[20:21], v[36:37] neg_lo:[0,1] neg_hi:[0,1]
	s_nop 0
	v_pk_mul_f32 v[66:67], v[40:41], v[220:221] op_sel:[1,1] op_sel_hi:[1,0] neg_lo:[1,0]
	s_nop 0
	v_pk_fma_f32 v[40:41], v[40:41], v[220:221], v[66:67] op_sel_hi:[0,1,1]
	v_pk_add_f32 v[36:37], v[22:23], v[40:41]
	v_pk_add_f32 v[22:23], v[22:23], v[40:41] neg_lo:[0,1] neg_hi:[0,1]
	s_nop 0
	v_pk_mul_f32 v[66:67], v[42:43], v[222:223] op_sel:[1,1] op_sel_hi:[1,0] neg_lo:[1,0]
	s_nop 0
	v_pk_fma_f32 v[42:43], v[42:43], v[222:223], v[66:67] op_sel_hi:[0,1,1]
	s_nop 0
	v_pk_mul_f32 v[66:67], v[46:47], v[224:225] op_sel:[1,1] op_sel_hi:[1,0] neg_lo:[1,0]
	s_nop 0
	v_pk_fma_f32 v[46:47], v[46:47], v[224:225], v[66:67] op_sel_hi:[0,1,1]
	s_nop 0
	v_pk_mul_f32 v[66:67], v[44:45], v[226:227] op_sel:[1,1] op_sel_hi:[1,0] neg_lo:[1,0]
	s_nop 0
	v_pk_fma_f32 v[44:45], v[44:45], v[226:227], v[66:67] op_sel_hi:[0,1,1]
	s_nop 0
	v_pk_mul_f32 v[66:67], v[48:49], v[228:229] op_sel:[1,1] op_sel_hi:[1,0] neg_lo:[1,0]
	s_nop 0
	v_pk_fma_f32 v[48:49], v[48:49], v[228:229], v[66:67] op_sel_hi:[0,1,1]
	s_nop 0
	v_pk_mul_f32 v[66:67], v[38:39], v[230:231] op_sel:[1,1] op_sel_hi:[1,0] neg_lo:[1,0]
	s_nop 0
	v_pk_fma_f32 v[38:39], v[38:39], v[230:231], v[66:67] op_sel_hi:[0,1,1]
	s_nop 0
	v_pk_mul_f32 v[64:65], v[18:19], v[232:233] op_sel:[1,1] op_sel_hi:[1,0] neg_lo:[1,0]
	v_mov_b32_e32 v66, v169
	v_pk_fma_f32 v[16:17], v[18:19], v[232:233], v[64:65] op_sel_hi:[0,1,1]
	v_mov_b32_e32 v64, v167
	v_mov_b32_e32 v18, v165
	s_nop 0
	s_nop 0
	v_pk_mul_f32 v[40:41], v[22:23], v[66:67] op_sel:[1,0] op_sel_hi:[0,0] neg_lo:[1,0]
	v_mov_b32_e32 v19, v171
	s_nop 0
	v_pk_fma_f32 v[22:23], v[22:23], v[18:19], v[40:41] op_sel_hi:[1,0,1]
	v_pk_add_f32 v[40:41], v[24:25], v[42:43]
	v_pk_add_f32 v[24:25], v[24:25], v[42:43] neg_lo:[0,1] neg_hi:[0,1]
	s_nop 0
	v_pk_mul_f32 v[42:43], v[24:25], v[64:65] op_sel:[1,0] op_sel_hi:[0,0] neg_lo:[1,0]
	s_nop 0
	v_pk_fma_f32 v[24:25], v[24:25], v[64:65], v[42:43] op_sel_hi:[1,0,1]
	v_pk_add_f32 v[42:43], v[26:27], v[46:47]
	v_pk_add_f32 v[26:27], v[26:27], v[46:47] neg_lo:[0,1] neg_hi:[0,1]
	s_nop 0
	v_pk_mul_f32 v[46:47], v[26:27], v[66:67] op_sel_hi:[1,0]
	s_nop 0
	v_pk_fma_f32 v[26:27], v[26:27], v[18:19], v[46:47] op_sel:[1,0,0] op_sel_hi:[0,0,1] neg_lo:[1,0,0]
	v_pk_add_f32 v[46:47], v[28:29], v[44:45]
	v_pk_add_f32 v[28:29], v[28:29], v[44:45] neg_lo:[0,1] neg_hi:[0,1]
	s_nop 0
	v_xor_b32_e32 v44, 0x80000000, v29
	v_mov_b32_e32 v45, v28
	v_pk_add_f32 v[28:29], v[30:31], v[48:49]
	v_pk_add_f32 v[30:31], v[30:31], v[48:49] neg_lo:[0,1] neg_hi:[0,1]
	s_nop 0
	v_pk_mul_f32 v[48:49], v[30:31], v[66:67] op_sel_hi:[1,0] neg_lo:[0,1] neg_hi:[0,1]
	s_nop 0
	v_pk_fma_f32 v[30:31], v[30:31], v[18:19], v[48:49] op_sel:[1,0,0] op_sel_hi:[0,0,1] neg_lo:[1,0,0]
	v_pk_add_f32 v[48:49], v[32:33], v[38:39]
	v_pk_add_f32 v[32:33], v[32:33], v[38:39] neg_lo:[0,1] neg_hi:[0,1]
	s_nop 0
	v_pk_mul_f32 v[38:39], v[32:33], v[64:65] op_sel:[1,0] op_sel_hi:[0,0] neg_lo:[1,0]
	s_nop 0
	v_pk_fma_f32 v[32:33], v[32:33], v[64:65], v[38:39] op_sel_hi:[1,0,1] neg_lo:[0,1,0] neg_hi:[0,1,0]
	v_pk_add_f32 v[38:39], v[34:35], v[16:17]
	v_pk_add_f32 v[16:17], v[34:35], v[16:17] neg_lo:[0,1] neg_hi:[0,1]
	s_nop 0
	v_pk_mul_f32 v[34:35], v[16:17], v[66:67] op_sel:[1,0] op_sel_hi:[0,0] neg_lo:[1,0]
	s_nop 0
	v_pk_fma_f32 v[16:17], v[16:17], v[18:19], v[34:35] op_sel_hi:[1,0,1] neg_lo:[0,1,0] neg_hi:[0,1,0]
	v_pk_add_f32 v[18:19], v[68:69], v[46:47]
	v_pk_add_f32 v[34:35], v[68:69], v[46:47] neg_lo:[0,1] neg_hi:[0,1]
	v_pk_add_f32 v[46:47], v[36:37], v[28:29]
	v_pk_add_f32 v[28:29], v[36:37], v[28:29] neg_lo:[0,1] neg_hi:[0,1]
	s_nop 0
	v_pk_mul_f32 v[36:37], v[28:29], v[64:65] op_sel:[1,0] op_sel_hi:[0,0] neg_lo:[1,0]
	s_nop 0
	v_pk_fma_f32 v[28:29], v[28:29], v[64:65], v[36:37] op_sel_hi:[1,0,1]
	v_pk_add_f32 v[36:37], v[40:41], v[48:49]
	v_pk_add_f32 v[40:41], v[40:41], v[48:49] neg_lo:[0,1] neg_hi:[0,1]
	s_nop 0
	v_xor_b32_e32 v48, 0x80000000, v41
	v_mov_b32_e32 v49, v40
	v_pk_add_f32 v[40:41], v[42:43], v[38:39]
	v_pk_add_f32 v[38:39], v[42:43], v[38:39] neg_lo:[0,1] neg_hi:[0,1]
	s_nop 0
	v_pk_mul_f32 v[42:43], v[64:65], v[38:39] op_sel:[0,1] op_sel_hi:[0,0] neg_lo:[0,1]
	v_pk_fma_f32 v[38:39], v[38:39], v[64:65], v[42:43] op_sel_hi:[1,0,1] neg_lo:[0,1,0] neg_hi:[0,1,0]
	v_pk_add_f32 v[42:43], v[18:19], v[36:37]
	v_pk_add_f32 v[18:19], v[18:19], v[36:37] neg_lo:[0,1] neg_hi:[0,1]
	v_pk_add_f32 v[36:37], v[46:47], v[40:41]
	v_pk_add_f32 v[40:41], v[46:47], v[40:41] neg_lo:[0,1] neg_hi:[0,1]
	s_nop 0
	v_xor_b32_e32 v46, 0x80000000, v41
	v_mov_b32_e32 v47, v40
	v_pk_add_f32 v[40:41], v[42:43], v[36:37]
	v_pk_add_f32 v[36:37], v[42:43], v[36:37] neg_lo:[0,1] neg_hi:[0,1]
	v_pk_add_f32 v[42:43], v[18:19], v[46:47]
	v_pk_add_f32 v[18:19], v[18:19], v[46:47] neg_lo:[0,1] neg_hi:[0,1]
	v_pk_add_f32 v[46:47], v[34:35], v[48:49]
	v_pk_add_f32 v[34:35], v[34:35], v[48:49] neg_lo:[0,1] neg_hi:[0,1]
	v_pk_add_f32 v[48:49], v[28:29], v[38:39]
	v_pk_add_f32 v[28:29], v[28:29], v[38:39] neg_lo:[0,1] neg_hi:[0,1]
	s_nop 0
	v_xor_b32_e32 v38, 0x80000000, v29
	v_mov_b32_e32 v39, v28
	v_pk_add_f32 v[28:29], v[46:47], v[48:49]
	v_pk_add_f32 v[46:47], v[46:47], v[48:49] neg_lo:[0,1] neg_hi:[0,1]
	v_pk_add_f32 v[48:49], v[34:35], v[38:39]
	v_pk_add_f32 v[34:35], v[34:35], v[38:39] neg_lo:[0,1] neg_hi:[0,1]
	v_pk_add_f32 v[38:39], v[20:21], v[44:45]
	v_pk_add_f32 v[20:21], v[20:21], v[44:45] neg_lo:[0,1] neg_hi:[0,1]
	v_pk_add_f32 v[44:45], v[22:23], v[30:31]
	v_pk_add_f32 v[22:23], v[22:23], v[30:31] neg_lo:[0,1] neg_hi:[0,1]
	s_nop 0
	v_pk_mul_f32 v[30:31], v[64:65], v[22:23] op_sel:[0,1] op_sel_hi:[0,0] neg_lo:[0,1]
	v_pk_fma_f32 v[22:23], v[64:65], v[22:23], v[30:31] op_sel_hi:[0,1,1]
	v_pk_add_f32 v[30:31], v[24:25], v[32:33]
	v_pk_add_f32 v[24:25], v[24:25], v[32:33] neg_lo:[0,1] neg_hi:[0,1]
	s_nop 0
	v_xor_b32_e32 v32, 0x80000000, v25
	v_mov_b32_e32 v33, v24
	v_pk_add_f32 v[24:25], v[26:27], v[16:17]
	v_pk_add_f32 v[16:17], v[26:27], v[16:17] neg_lo:[0,1] neg_hi:[0,1]
	s_nop 0
	v_pk_mul_f32 v[26:27], v[64:65], v[16:17] op_sel:[0,1] op_sel_hi:[0,0] neg_lo:[0,1]
	v_pk_fma_f32 v[16:17], v[64:65], v[16:17], v[26:27] op_sel_hi:[0,1,1] neg_lo:[1,0,0] neg_hi:[1,0,0]
	v_pk_add_f32 v[26:27], v[38:39], v[30:31]
	v_pk_add_f32 v[30:31], v[38:39], v[30:31] neg_lo:[0,1] neg_hi:[0,1]
	v_pk_add_f32 v[38:39], v[44:45], v[24:25]
	v_pk_add_f32 v[24:25], v[44:45], v[24:25] neg_lo:[0,1] neg_hi:[0,1]
	s_nop 0
	v_xor_b32_e32 v44, 0x80000000, v25
	v_mov_b32_e32 v45, v24
	v_pk_add_f32 v[24:25], v[26:27], v[38:39]
	v_pk_add_f32 v[26:27], v[26:27], v[38:39] neg_lo:[0,1] neg_hi:[0,1]
	v_pk_add_f32 v[38:39], v[30:31], v[44:45]
	v_pk_add_f32 v[30:31], v[30:31], v[44:45] neg_lo:[0,1] neg_hi:[0,1]
	v_pk_add_f32 v[44:45], v[20:21], v[32:33]
	v_pk_add_f32 v[20:21], v[20:21], v[32:33] neg_lo:[0,1] neg_hi:[0,1]
	v_pk_add_f32 v[32:33], v[22:23], v[16:17]
	v_pk_add_f32 v[16:17], v[22:23], v[16:17] neg_lo:[0,1] neg_hi:[0,1]
	s_nop 0
	v_xor_b32_e32 v22, 0x80000000, v17
	v_mov_b32_e32 v23, v16
	v_pk_add_f32 v[16:17], v[44:45], v[32:33]
	v_pk_add_f32 v[32:33], v[44:45], v[32:33] neg_lo:[0,1] neg_hi:[0,1]
	v_pk_add_f32 v[44:45], v[20:21], v[22:23]
	v_pk_add_f32 v[20:21], v[20:21], v[22:23] neg_lo:[0,1] neg_hi:[0,1]
	ds_write_b64 v10, v[40:41]
	ds_write_b64 v13, v[24:25]
	ds_write_b64 v15, v[28:29]
	ds_write_b64 v50, v[16:17]
	ds_write_b64 v51, v[42:43]
	ds_write_b64 v52, v[38:39]
	ds_write_b64 v53, v[48:49]
	ds_write_b64 v54, v[44:45]
	ds_write_b64 v55, v[36:37]
	ds_write_b64 v56, v[26:27]
	ds_write_b64 v57, v[46:47]
	ds_write_b64 v58, v[32:33]
	ds_write_b64 v59, v[18:19]
	ds_write_b64 v60, v[30:31]
	ds_write_b64 v61, v[34:35]
	ds_write_b64 v62, v[20:21]
	v_mov_b32_e32 v10, v174
	v_mov_b32_e32 v50, v172
	s_waitcnt lgkmcnt(0)
	s_barrier
	v_add_u32_e32 v13, v50, v10
	v_lshl_add_u32 v13, v13, 3, 0
	ds_read2_b64 v[16:19], v13 offset1:16
	v_xad_u32 v15, v50, 1, v10
	v_lshl_add_u32 v15, v15, 3, 0
	s_waitcnt lgkmcnt(0)
	v_pk_fma_f32 v[16:17], v[16:17], 0, v[16:17] op_sel:[1,0,0] op_sel_hi:[0,0,1] neg_hi:[1,0,0]
	v_pk_fma_f32 v[22:23], v[180:181], s[90:91], v[180:181] op_sel:[1,0,0] op_sel_hi:[0,1,1]
	v_pk_mul_f32 v[24:25], v[22:23], v[18:19] op_sel:[1,1] op_sel_hi:[1,0] neg_hi:[0,1]
	s_nop 0
	v_pk_fma_f32 v[18:19], v[18:19], v[22:23], v[24:25] op_sel_hi:[1,0,1]
	v_pk_mul_f32 v[24:25], v[180:181], v[22:23] op_sel:[1,1] op_sel_hi:[0,1] neg_lo:[0,1]
	v_pk_fma_f32 v[26:27], v[180:181], v[22:23], v[24:25] op_sel_hi:[1,0,1]
	ds_read2_b64 v[22:25], v15 offset0:32 offset1:48
	s_waitcnt lgkmcnt(0)
	v_pk_mul_f32 v[28:29], v[22:23], v[26:27] op_sel:[1,1] op_sel_hi:[0,1] neg_hi:[1,0]
	s_nop 0
	v_pk_fma_f32 v[22:23], v[22:23], v[26:27], v[28:29] op_sel_hi:[1,0,1]
	v_pk_mul_f32 v[28:29], v[180:181], v[26:27] op_sel:[1,1] op_sel_hi:[0,1] neg_lo:[0,1]
	v_pk_fma_f32 v[26:27], v[180:181], v[26:27], v[28:29] op_sel_hi:[1,0,1]
	s_nop 0
	v_pk_mul_f32 v[28:29], v[24:25], v[26:27] op_sel:[1,1] op_sel_hi:[0,1] neg_hi:[1,0]
	s_nop 0
	v_pk_fma_f32 v[24:25], v[24:25], v[26:27], v[28:29] op_sel_hi:[1,0,1]
	v_pk_mul_f32 v[28:29], v[180:181], v[26:27] op_sel:[1,1] op_sel_hi:[0,1] neg_lo:[0,1]
	v_pk_fma_f32 v[26:27], v[180:181], v[26:27], v[28:29] op_sel_hi:[1,0,1]
	v_xad_u32 v28, v50, 2, v10
	v_lshl_add_u32 v51, v28, 3, 0
	ds_read2_b64 v[28:31], v51 offset0:64 offset1:80
	v_pk_mul_f32 v[32:33], v[180:181], v[26:27] op_sel:[1,1] op_sel_hi:[0,1] neg_lo:[0,1]
	s_waitcnt lgkmcnt(0)
	v_pk_mul_f32 v[34:35], v[28:29], v[26:27] op_sel:[1,1] op_sel_hi:[0,1] neg_hi:[1,0]
	s_nop 0
	v_pk_fma_f32 v[28:29], v[28:29], v[26:27], v[34:35] op_sel_hi:[1,0,1]
	v_pk_fma_f32 v[34:35], v[180:181], v[26:27], v[32:33] op_sel_hi:[1,0,1]
	s_nop 0
	v_pk_mul_f32 v[26:27], v[30:31], v[34:35] op_sel:[1,1] op_sel_hi:[0,1] neg_hi:[1,0]
	v_pk_fma_f32 v[26:27], v[30:31], v[34:35], v[26:27] op_sel_hi:[1,0,1]
	v_xad_u32 v30, v50, 3, v10
	v_lshl_add_u32 v54, v30, 3, 0
	ds_read2_b64 v[30:33], v54 offset0:96 offset1:112
	v_pk_mul_f32 v[36:37], v[180:181], v[34:35] op_sel:[1,1] op_sel_hi:[0,1] neg_lo:[0,1]
	v_pk_fma_f32 v[34:35], v[180:181], v[34:35], v[36:37] op_sel_hi:[1,0,1]
	s_waitcnt lgkmcnt(0)
	v_pk_mul_f32 v[36:37], v[30:31], v[34:35] op_sel:[1,1] op_sel_hi:[0,1] neg_hi:[1,0]
	s_nop 0
	v_pk_fma_f32 v[30:31], v[30:31], v[34:35], v[36:37] op_sel_hi:[1,0,1]
	v_pk_mul_f32 v[36:37], v[180:181], v[34:35] op_sel:[1,1] op_sel_hi:[0,1] neg_lo:[0,1]
	v_pk_fma_f32 v[34:35], v[180:181], v[34:35], v[36:37] op_sel_hi:[1,0,1]
	s_nop 0
	v_pk_mul_f32 v[36:37], v[32:33], v[34:35] op_sel:[1,1] op_sel_hi:[0,1] neg_hi:[1,0]
	s_nop 0
	v_pk_fma_f32 v[32:33], v[32:33], v[34:35], v[36:37] op_sel_hi:[1,0,1]
	v_pk_mul_f32 v[36:37], v[180:181], v[34:35] op_sel:[1,1] op_sel_hi:[0,1] neg_lo:[0,1]
	v_pk_fma_f32 v[38:39], v[180:181], v[34:35], v[36:37] op_sel_hi:[1,0,1]
	v_xad_u32 v34, v50, 4, v10
	v_lshl_add_u32 v55, v34, 3, 0
	ds_read2_b64 v[34:37], v55 offset0:128 offset1:144
	v_pk_mul_f32 v[40:41], v[180:181], v[38:39] op_sel:[1,1] op_sel_hi:[0,1] neg_lo:[0,1]
	s_waitcnt lgkmcnt(0)
	v_pk_mul_f32 v[42:43], v[34:35], v[38:39] op_sel:[1,1] op_sel_hi:[0,1] neg_hi:[1,0]
	s_nop 0
	v_pk_fma_f32 v[34:35], v[34:35], v[38:39], v[42:43] op_sel_hi:[1,0,1]
	v_pk_fma_f32 v[42:43], v[180:181], v[38:39], v[40:41] op_sel_hi:[1,0,1]
	s_nop 0
	v_pk_mul_f32 v[38:39], v[36:37], v[42:43] op_sel:[1,1] op_sel_hi:[0,1] neg_hi:[1,0]
	v_pk_fma_f32 v[36:37], v[36:37], v[42:43], v[38:39] op_sel_hi:[1,0,1]
	v_xad_u32 v38, v50, 5, v10
	v_lshl_add_u32 v56, v38, 3, 0
	ds_read2_b64 v[38:41], v56 offset0:160 offset1:176
	v_pk_mul_f32 v[44:45], v[180:181], v[42:43] op_sel:[1,1] op_sel_hi:[0,1] neg_lo:[0,1]
	v_pk_fma_f32 v[42:43], v[180:181], v[42:43], v[44:45] op_sel_hi:[1,0,1]
	s_waitcnt lgkmcnt(0)
	v_pk_mul_f32 v[44:45], v[38:39], v[42:43] op_sel:[1,1] op_sel_hi:[0,1] neg_hi:[1,0]
	s_nop 0
	v_pk_fma_f32 v[38:39], v[38:39], v[42:43], v[44:45] op_sel_hi:[1,0,1]
	v_pk_mul_f32 v[44:45], v[180:181], v[42:43] op_sel:[1,1] op_sel_hi:[0,1] neg_lo:[0,1]
	v_pk_fma_f32 v[42:43], v[180:181], v[42:43], v[44:45] op_sel_hi:[1,0,1]
	s_nop 0
	v_pk_mul_f32 v[44:45], v[40:41], v[42:43] op_sel:[1,1] op_sel_hi:[0,1] neg_hi:[1,0]
	s_nop 0
	v_pk_fma_f32 v[40:41], v[40:41], v[42:43], v[44:45] op_sel_hi:[1,0,1]
	v_pk_mul_f32 v[44:45], v[180:181], v[42:43] op_sel:[1,1] op_sel_hi:[0,1] neg_lo:[0,1]
	v_pk_fma_f32 v[42:43], v[180:181], v[42:43], v[44:45] op_sel_hi:[1,0,1]
	v_xad_u32 v44, v50, 6, v10
	v_lshl_add_u32 v57, v44, 3, 0
	ds_read2_b64 v[44:47], v57 offset0:192 offset1:208
	v_pk_mul_f32 v[48:49], v[180:181], v[42:43] op_sel:[1,1] op_sel_hi:[0,1] neg_lo:[0,1]
	s_waitcnt lgkmcnt(0)
	v_pk_mul_f32 v[52:53], v[44:45], v[42:43] op_sel:[1,1] op_sel_hi:[0,1] neg_hi:[1,0]
	s_nop 0
	v_pk_fma_f32 v[44:45], v[44:45], v[42:43], v[52:53] op_sel_hi:[1,0,1]
	v_pk_fma_f32 v[52:53], v[180:181], v[42:43], v[48:49] op_sel_hi:[1,0,1]
	s_nop 0
	v_pk_mul_f32 v[42:43], v[46:47], v[52:53] op_sel:[1,1] op_sel_hi:[0,1] neg_hi:[1,0]
	v_pk_fma_f32 v[42:43], v[46:47], v[52:53], v[42:43] op_sel_hi:[1,0,1]
	v_xad_u32 v46, v50, 7, v10
	v_lshl_add_u32 v58, v46, 3, 0
	ds_read2_b64 v[46:49], v58 offset0:224 offset1:240
	v_pk_mul_f32 v[60:61], v[180:181], v[52:53] op_sel:[1,1] op_sel_hi:[0,1] neg_lo:[0,1]
	v_pk_fma_f32 v[52:53], v[180:181], v[52:53], v[60:61] op_sel_hi:[1,0,1]
	s_waitcnt lgkmcnt(0)
	v_pk_mul_f32 v[60:61], v[46:47], v[52:53] op_sel:[1,1] op_sel_hi:[0,1] neg_hi:[1,0]
	s_nop 0
	v_pk_fma_f32 v[46:47], v[46:47], v[52:53], v[60:61] op_sel_hi:[1,0,1]
	v_pk_mul_f32 v[60:61], v[180:181], v[52:53] op_sel:[1,1] op_sel_hi:[0,1] neg_lo:[0,1]
	v_pk_fma_f32 v[52:53], v[180:181], v[52:53], v[60:61] op_sel_hi:[1,0,1]
	s_nop 0
	v_pk_mul_f32 v[60:61], v[48:49], v[52:53] op_sel:[1,1] op_sel_hi:[0,1] neg_hi:[1,0]
	s_nop 0
	v_pk_fma_f32 v[48:49], v[48:49], v[52:53], v[60:61] op_sel_hi:[1,0,1]
	v_pk_mul_f32 v[60:61], v[180:181], v[52:53] op_sel:[1,1] op_sel_hi:[0,1] neg_lo:[0,1]
	v_pk_fma_f32 v[64:65], v[180:181], v[52:53], v[60:61] op_sel_hi:[1,0,1]
	v_xad_u32 v52, v50, 8, v10
	v_lshl_add_u32 v52, v52, 3, 0
	v_add_u32_e32 v59, 0x800, v52
	ds_read2_b64 v[60:63], v59 offset1:16
	v_pk_mul_f32 v[66:67], v[180:181], v[64:65] op_sel:[1,1] op_sel_hi:[0,1] neg_lo:[0,1]
	v_pk_fma_f32 v[66:67], v[180:181], v[64:65], v[66:67] op_sel_hi:[1,0,1]
	s_waitcnt lgkmcnt(0)
	v_pk_mul_f32 v[52:53], v[60:61], v[64:65] op_sel:[1,1] op_sel_hi:[0,1] neg_hi:[1,0]
	v_pk_fma_f32 v[52:53], v[60:61], v[64:65], v[52:53] op_sel_hi:[1,0,1]
	v_pk_mul_f32 v[60:61], v[62:63], v[66:67] op_sel:[1,1] op_sel_hi:[0,1] neg_hi:[1,0]
	v_pk_fma_f32 v[70:71], v[62:63], v[66:67], v[60:61] op_sel_hi:[1,0,1]
	v_xad_u32 v60, v50, 9, v10
	v_lshl_add_u32 v60, v60, 3, 0
	v_add_u32_e32 v60, 0x800, v60
	ds_read2_b64 v[62:65], v60 offset0:32 offset1:48
	v_pk_mul_f32 v[68:69], v[180:181], v[66:67] op_sel:[1,1] op_sel_hi:[0,1] neg_lo:[0,1]
	v_pk_fma_f32 v[66:67], v[180:181], v[66:67], v[68:69] op_sel_hi:[1,0,1]
	s_waitcnt lgkmcnt(0)
	v_pk_mul_f32 v[68:69], v[62:63], v[66:67] op_sel:[1,1] op_sel_hi:[0,1] neg_hi:[1,0]
	s_nop 0
	v_pk_fma_f32 v[72:73], v[62:63], v[66:67], v[68:69] op_sel_hi:[1,0,1]
	v_pk_mul_f32 v[62:63], v[180:181], v[66:67] op_sel:[1,1] op_sel_hi:[0,1] neg_lo:[0,1]
	v_pk_fma_f32 v[62:63], v[180:181], v[66:67], v[62:63] op_sel_hi:[1,0,1]
	s_nop 0
	v_pk_mul_f32 v[66:67], v[64:65], v[62:63] op_sel:[1,1] op_sel_hi:[0,1] neg_hi:[1,0]
	s_nop 0
	v_pk_fma_f32 v[74:75], v[64:65], v[62:63], v[66:67] op_sel_hi:[1,0,1]
	v_pk_mul_f32 v[64:65], v[180:181], v[62:63] op_sel:[1,1] op_sel_hi:[0,1] neg_lo:[0,1]
	v_pk_fma_f32 v[66:67], v[180:181], v[62:63], v[64:65] op_sel_hi:[1,0,1]
	v_xad_u32 v61, v50, 10, v10
	v_lshl_add_u32 v61, v61, 3, 0
	v_add_u32_e32 v61, 0x800, v61
	ds_read2_b64 v[62:65], v61 offset0:64 offset1:80
	v_pk_mul_f32 v[68:69], v[180:181], v[66:67] op_sel:[1,1] op_sel_hi:[0,1] neg_lo:[0,1]
	v_pk_fma_f32 v[68:69], v[180:181], v[66:67], v[68:69] op_sel_hi:[1,0,1]
	s_waitcnt lgkmcnt(0)
	v_pk_mul_f32 v[76:77], v[62:63], v[66:67] op_sel:[1,1] op_sel_hi:[0,1] neg_hi:[1,0]
	v_pk_fma_f32 v[76:77], v[62:63], v[66:67], v[76:77] op_sel_hi:[1,0,1]
	v_pk_mul_f32 v[62:63], v[64:65], v[68:69] op_sel:[1,1] op_sel_hi:[0,1] neg_hi:[1,0]
	v_pk_fma_f32 v[78:79], v[64:65], v[68:69], v[62:63] op_sel_hi:[1,0,1]
	v_xad_u32 v62, v50, 11, v10
	v_lshl_add_u32 v62, v62, 3, 0
	v_add_u32_e32 v62, 0x800, v62
	ds_read2_b64 v[64:67], v62 offset0:96 offset1:112
	v_pk_mul_f32 v[80:81], v[180:181], v[68:69] op_sel:[1,1] op_sel_hi:[0,1] neg_lo:[0,1]
	v_pk_fma_f32 v[68:69], v[180:181], v[68:69], v[80:81] op_sel_hi:[1,0,1]
	s_waitcnt lgkmcnt(0)
	v_pk_mul_f32 v[80:81], v[64:65], v[68:69] op_sel:[1,1] op_sel_hi:[0,1] neg_hi:[1,0]
	s_nop 0
	v_pk_fma_f32 v[80:81], v[64:65], v[68:69], v[80:81] op_sel_hi:[1,0,1]
	v_pk_mul_f32 v[64:65], v[180:181], v[68:69] op_sel:[1,1] op_sel_hi:[0,1] neg_lo:[0,1]
	v_pk_fma_f32 v[64:65], v[180:181], v[68:69], v[64:65] op_sel_hi:[1,0,1]
	s_nop 0
	v_pk_mul_f32 v[68:69], v[66:67], v[64:65] op_sel:[1,1] op_sel_hi:[0,1] neg_hi:[1,0]
	s_nop 0
	v_pk_fma_f32 v[82:83], v[66:67], v[64:65], v[68:69] op_sel_hi:[1,0,1]
	v_pk_mul_f32 v[66:67], v[180:181], v[64:65] op_sel:[1,1] op_sel_hi:[0,1] neg_lo:[0,1]
	v_pk_fma_f32 v[68:69], v[180:181], v[64:65], v[66:67] op_sel_hi:[1,0,1]
	v_xad_u32 v63, v50, 12, v10
	v_lshl_add_u32 v63, v63, 3, 0
	v_add_u32_e32 v63, 0x800, v63
	ds_read2_b64 v[64:67], v63 offset0:128 offset1:144
	v_pk_mul_f32 v[84:85], v[180:181], v[68:69] op_sel:[1,1] op_sel_hi:[0,1] neg_lo:[0,1]
	v_pk_fma_f32 v[84:85], v[180:181], v[68:69], v[84:85] op_sel_hi:[1,0,1]
	s_waitcnt lgkmcnt(0)
	v_pk_mul_f32 v[86:87], v[64:65], v[68:69] op_sel:[1,1] op_sel_hi:[0,1] neg_hi:[1,0]
	v_pk_fma_f32 v[86:87], v[64:65], v[68:69], v[86:87] op_sel_hi:[1,0,1]
	v_pk_mul_f32 v[64:65], v[66:67], v[84:85] op_sel:[1,1] op_sel_hi:[0,1] neg_hi:[1,0]
	v_pk_fma_f32 v[88:89], v[66:67], v[84:85], v[64:65] op_sel_hi:[1,0,1]
	v_xad_u32 v64, v50, 13, v10
	v_lshl_add_u32 v64, v64, 3, 0
	v_add_u32_e32 v64, 0x800, v64
	ds_read2_b64 v[66:69], v64 offset0:160 offset1:176
	v_pk_mul_f32 v[90:91], v[180:181], v[84:85] op_sel:[1,1] op_sel_hi:[0,1] neg_lo:[0,1]
	v_pk_fma_f32 v[84:85], v[180:181], v[84:85], v[90:91] op_sel_hi:[1,0,1]
	s_waitcnt lgkmcnt(0)
	v_pk_mul_f32 v[90:91], v[66:67], v[84:85] op_sel:[1,1] op_sel_hi:[0,1] neg_hi:[1,0]
	s_nop 0
	v_pk_fma_f32 v[90:91], v[66:67], v[84:85], v[90:91] op_sel_hi:[1,0,1]
	v_pk_mul_f32 v[66:67], v[180:181], v[84:85] op_sel:[1,1] op_sel_hi:[0,1] neg_lo:[0,1]
	v_pk_fma_f32 v[66:67], v[180:181], v[84:85], v[66:67] op_sel_hi:[1,0,1]
	s_nop 0
	v_pk_mul_f32 v[84:85], v[68:69], v[66:67] op_sel:[1,1] op_sel_hi:[0,1] neg_hi:[1,0]
	s_nop 0
	v_pk_fma_f32 v[84:85], v[68:69], v[66:67], v[84:85] op_sel_hi:[1,0,1]
	v_pk_mul_f32 v[68:69], v[180:181], v[66:67] op_sel:[1,1] op_sel_hi:[0,1] neg_lo:[0,1]
	v_pk_fma_f32 v[92:93], v[180:181], v[66:67], v[68:69] op_sel_hi:[1,0,1]
	v_xad_u32 v65, v50, 14, v10
	v_lshl_add_u32 v65, v65, 3, 0
	v_add_u32_e32 v65, 0x800, v65
	ds_read2_b64 v[66:69], v65 offset0:192 offset1:208
	v_pk_mul_f32 v[94:95], v[180:181], v[92:93] op_sel:[1,1] op_sel_hi:[0,1] neg_lo:[0,1]
	v_xad_u32 v10, v50, 15, v10
	s_waitcnt lgkmcnt(0)
	v_pk_mul_f32 v[96:97], v[66:67], v[92:93] op_sel:[1,1] op_sel_hi:[0,1] neg_hi:[1,0]
	v_lshl_add_u32 v10, v10, 3, 0
	v_pk_fma_f32 v[96:97], v[66:67], v[92:93], v[96:97] op_sel_hi:[1,0,1]
	v_pk_fma_f32 v[92:93], v[180:181], v[92:93], v[94:95] op_sel_hi:[1,0,1]
	s_nop 0
	v_pk_mul_f32 v[66:67], v[68:69], v[92:93] op_sel:[1,1] op_sel_hi:[0,1] neg_hi:[1,0]
	v_add_u32_e32 v101, 0x800, v10
	v_pk_fma_f32 v[94:95], v[68:69], v[92:93], v[66:67] op_sel_hi:[1,0,1]
	ds_read2_b64 v[66:69], v101 offset0:224 offset1:240
	v_pk_mul_f32 v[98:99], v[180:181], v[92:93] op_sel:[1,1] op_sel_hi:[0,1] neg_lo:[0,1]
	v_pk_fma_f32 v[92:93], v[180:181], v[92:93], v[98:99] op_sel_hi:[1,0,1]
	s_waitcnt lgkmcnt(0)
	v_pk_mul_f32 v[98:99], v[66:67], v[92:93] op_sel:[1,1] op_sel_hi:[0,1] neg_hi:[1,0]
	s_nop 0
	v_pk_fma_f32 v[66:67], v[66:67], v[92:93], v[98:99] op_sel_hi:[1,0,1]
	v_pk_mul_f32 v[98:99], v[180:181], v[92:93] op_sel:[1,1] op_sel_hi:[0,1] neg_lo:[0,1]
	v_pk_fma_f32 v[20:21], v[180:181], v[92:93], v[98:99] op_sel_hi:[1,0,1]
	s_nop 0
	v_pk_mul_f32 v[92:93], v[68:69], v[20:21] op_sel:[1,1] op_sel_hi:[0,1] neg_hi:[1,0]
	s_nop 0
	v_pk_fma_f32 v[68:69], v[68:69], v[20:21], v[92:93] op_sel_hi:[1,0,1]
	v_pk_add_f32 v[104:105], v[16:17], v[52:53]
	v_pk_add_f32 v[16:17], v[16:17], v[52:53] neg_lo:[0,1] neg_hi:[0,1]
	v_pk_add_f32 v[52:53], v[18:19], v[70:71]
	v_pk_add_f32 v[18:19], v[18:19], v[70:71] neg_lo:[0,1] neg_hi:[0,1]
	v_mov_b32_e32 v92, v164
	v_mov_b32_e32 v20, v165
	v_mov_b32_e32 v98, v166
	v_mov_b32_e32 v10, v167
	v_mov_b32_e32 v100, v168
	v_mov_b32_e32 v50, v169
	v_mov_b32_e32 v102, v170
	v_mov_b32_e32 v21, v171
	v_pk_mul_f32 v[70:71], v[102:103], v[18:19] op_sel:[0,1] op_sel_hi:[0,0] neg_lo:[0,1]
	v_pk_fma_f32 v[18:19], v[92:93], v[18:19], v[70:71] op_sel_hi:[0,1,1]
	v_pk_add_f32 v[70:71], v[22:23], v[72:73]
	v_pk_add_f32 v[22:23], v[22:23], v[72:73] neg_lo:[0,1] neg_hi:[0,1]
	s_nop 0
	v_pk_mul_f32 v[72:73], v[50:51], v[22:23] op_sel:[0,1] op_sel_hi:[0,0] neg_lo:[0,1]
	v_pk_fma_f32 v[22:23], v[20:21], v[22:23], v[72:73] op_sel_hi:[0,1,1]
	v_pk_add_f32 v[72:73], v[24:25], v[74:75]
	v_pk_add_f32 v[24:25], v[24:25], v[74:75] neg_lo:[0,1] neg_hi:[0,1]
	s_nop 0
	v_pk_mul_f32 v[74:75], v[100:101], v[24:25] op_sel:[0,1] op_sel_hi:[0,0] neg_lo:[0,1]
	v_pk_fma_f32 v[24:25], v[98:99], v[24:25], v[74:75] op_sel_hi:[0,1,1]
	v_pk_add_f32 v[74:75], v[28:29], v[76:77]
	v_pk_add_f32 v[28:29], v[28:29], v[76:77] neg_lo:[0,1] neg_hi:[0,1]
	s_nop 0
	v_pk_mul_f32 v[76:77], v[10:11], v[28:29] op_sel:[0,1] op_sel_hi:[0,0] neg_lo:[0,1]
	v_pk_fma_f32 v[28:29], v[10:11], v[28:29], v[76:77] op_sel_hi:[0,1,1]
	v_pk_add_f32 v[76:77], v[26:27], v[78:79]
	v_pk_add_f32 v[26:27], v[26:27], v[78:79] neg_lo:[0,1] neg_hi:[0,1]
	s_nop 0
	v_pk_mul_f32 v[78:79], v[98:99], v[26:27] op_sel:[0,1] op_sel_hi:[0,0] neg_lo:[0,1]
	v_pk_fma_f32 v[26:27], v[100:101], v[26:27], v[78:79] op_sel_hi:[0,1,1]
	v_pk_add_f32 v[78:79], v[30:31], v[80:81]
	v_pk_add_f32 v[30:31], v[30:31], v[80:81] neg_lo:[0,1] neg_hi:[0,1]
	s_nop 0
	v_pk_mul_f32 v[80:81], v[20:21], v[30:31] op_sel:[0,1] op_sel_hi:[0,0] neg_lo:[0,1]
	v_pk_fma_f32 v[30:31], v[50:51], v[30:31], v[80:81] op_sel_hi:[0,1,1]
	v_pk_add_f32 v[80:81], v[32:33], v[82:83]
	v_pk_add_f32 v[32:33], v[32:33], v[82:83] neg_lo:[0,1] neg_hi:[0,1]
	s_nop 0
	v_pk_mul_f32 v[82:83], v[92:93], v[32:33] op_sel:[0,1] op_sel_hi:[0,0] neg_lo:[0,1]
	v_pk_fma_f32 v[32:33], v[102:103], v[32:33], v[82:83] op_sel_hi:[0,1,1]
	v_pk_add_f32 v[82:83], v[34:35], v[86:87]
	v_pk_add_f32 v[34:35], v[34:35], v[86:87] neg_lo:[0,1] neg_hi:[0,1]
	s_nop 0
	v_xor_b32_e32 v86, 0x80000000, v35
	v_mov_b32_e32 v87, v34
	v_pk_add_f32 v[34:35], v[36:37], v[88:89]
	v_pk_add_f32 v[36:37], v[36:37], v[88:89] neg_lo:[0,1] neg_hi:[0,1]
	s_nop 0
	v_pk_mul_f32 v[88:89], v[92:93], v[36:37] op_sel:[0,1] op_sel_hi:[0,0] neg_lo:[0,1]
	v_pk_fma_f32 v[36:37], v[102:103], v[36:37], v[88:89] op_sel_hi:[0,1,1] neg_lo:[1,0,0] neg_hi:[1,0,0]
	v_pk_add_f32 v[88:89], v[38:39], v[90:91]
	v_pk_add_f32 v[38:39], v[38:39], v[90:91] neg_lo:[0,1] neg_hi:[0,1]
	s_nop 0
	v_pk_mul_f32 v[90:91], v[20:21], v[38:39] op_sel:[0,1] op_sel_hi:[0,0] neg_lo:[0,1]
	v_pk_fma_f32 v[38:39], v[50:51], v[38:39], v[90:91] op_sel_hi:[0,1,1] neg_lo:[1,0,0] neg_hi:[1,0,0]
	v_pk_add_f32 v[90:91], v[40:41], v[84:85]
	v_pk_add_f32 v[40:41], v[40:41], v[84:85] neg_lo:[0,1] neg_hi:[0,1]
	s_nop 0
	v_pk_mul_f32 v[84:85], v[98:99], v[40:41] op_sel:[0,1] op_sel_hi:[0,0] neg_lo:[0,1]
	v_pk_fma_f32 v[40:41], v[100:101], v[40:41], v[84:85] op_sel_hi:[0,1,1] neg_lo:[1,0,0] neg_hi:[1,0,0]
	v_pk_add_f32 v[84:85], v[44:45], v[96:97]
	v_pk_add_f32 v[44:45], v[44:45], v[96:97] neg_lo:[0,1] neg_hi:[0,1]
	s_nop 0
	v_pk_mul_f32 v[96:97], v[10:11], v[44:45] op_sel:[0,1] op_sel_hi:[0,0] neg_lo:[0,1]
	v_pk_fma_f32 v[44:45], v[10:11], v[44:45], v[96:97] op_sel_hi:[0,1,1] neg_lo:[1,0,0] neg_hi:[1,0,0]
	v_pk_add_f32 v[96:97], v[42:43], v[94:95]
	v_pk_add_f32 v[42:43], v[42:43], v[94:95] neg_lo:[0,1] neg_hi:[0,1]
	s_nop 0
	v_pk_mul_f32 v[94:95], v[100:101], v[42:43] op_sel:[0,1] op_sel_hi:[0,0] neg_lo:[0,1]
	v_pk_fma_f32 v[42:43], v[98:99], v[42:43], v[94:95] op_sel_hi:[0,1,1] neg_lo:[1,0,0] neg_hi:[1,0,0]
	v_pk_add_f32 v[94:95], v[46:47], v[66:67]
	v_pk_add_f32 v[46:47], v[46:47], v[66:67] neg_lo:[0,1] neg_hi:[0,1]
	s_nop 0
	v_pk_mul_f32 v[66:67], v[50:51], v[46:47] op_sel:[0,1] op_sel_hi:[0,0] neg_lo:[0,1]
	v_pk_fma_f32 v[46:47], v[20:21], v[46:47], v[66:67] op_sel_hi:[0,1,1] neg_lo:[1,0,0] neg_hi:[1,0,0]
	v_pk_add_f32 v[66:67], v[48:49], v[68:69]
	v_pk_add_f32 v[48:49], v[48:49], v[68:69] neg_lo:[0,1] neg_hi:[0,1]
	s_nop 0
	v_pk_mul_f32 v[68:69], v[102:103], v[48:49] op_sel:[0,1] op_sel_hi:[0,0] neg_lo:[0,1]
	v_pk_fma_f32 v[48:49], v[92:93], v[48:49], v[68:69] op_sel_hi:[0,1,1] neg_lo:[1,0,0] neg_hi:[1,0,0]
	v_pk_add_f32 v[92:93], v[52:53], v[34:35]
	v_pk_add_f32 v[34:35], v[52:53], v[34:35] neg_lo:[0,1] neg_hi:[0,1]
	v_pk_add_f32 v[68:69], v[104:105], v[82:83]
	v_pk_mul_f32 v[52:53], v[50:51], v[34:35] op_sel:[0,1] op_sel_hi:[0,0] neg_lo:[0,1]
	v_pk_fma_f32 v[34:35], v[20:21], v[34:35], v[52:53] op_sel_hi:[0,1,1]
	v_pk_add_f32 v[52:53], v[70:71], v[88:89]
	v_pk_add_f32 v[70:71], v[70:71], v[88:89] neg_lo:[0,1] neg_hi:[0,1]
	v_pk_add_f32 v[82:83], v[104:105], v[82:83] neg_lo:[0,1] neg_hi:[0,1]
	v_pk_mul_f32 v[88:89], v[10:11], v[70:71] op_sel:[0,1] op_sel_hi:[0,0] neg_lo:[0,1]
	v_pk_fma_f32 v[70:71], v[10:11], v[70:71], v[88:89] op_sel_hi:[0,1,1]
	v_pk_add_f32 v[88:89], v[72:73], v[90:91]
	v_pk_add_f32 v[72:73], v[72:73], v[90:91] neg_lo:[0,1] neg_hi:[0,1]
	s_nop 0
	v_pk_mul_f32 v[90:91], v[20:21], v[72:73] op_sel:[0,1] op_sel_hi:[0,0] neg_lo:[0,1]
	v_pk_fma_f32 v[72:73], v[50:51], v[72:73], v[90:91] op_sel_hi:[0,1,1]
	v_pk_add_f32 v[90:91], v[74:75], v[84:85]
	v_pk_add_f32 v[74:75], v[74:75], v[84:85] neg_lo:[0,1] neg_hi:[0,1]
	s_nop 0
	v_xor_b32_e32 v84, 0x80000000, v75
	v_mov_b32_e32 v85, v74
	v_pk_add_f32 v[74:75], v[76:77], v[96:97]
	v_pk_add_f32 v[76:77], v[76:77], v[96:97] neg_lo:[0,1] neg_hi:[0,1]
	s_nop 0
	v_pk_mul_f32 v[96:97], v[20:21], v[76:77] op_sel:[0,1] op_sel_hi:[0,0] neg_lo:[0,1]
	v_pk_fma_f32 v[76:77], v[50:51], v[76:77], v[96:97] op_sel_hi:[0,1,1] neg_lo:[1,0,0] neg_hi:[1,0,0]
	v_pk_add_f32 v[96:97], v[78:79], v[94:95]
	v_pk_add_f32 v[78:79], v[78:79], v[94:95] neg_lo:[0,1] neg_hi:[0,1]
	s_nop 0
	v_pk_mul_f32 v[94:95], v[10:11], v[78:79] op_sel:[0,1] op_sel_hi:[0,0] neg_lo:[0,1]
	v_pk_fma_f32 v[78:79], v[10:11], v[78:79], v[94:95] op_sel_hi:[0,1,1] neg_lo:[1,0,0] neg_hi:[1,0,0]
	v_pk_add_f32 v[94:95], v[80:81], v[66:67]
	v_pk_add_f32 v[66:67], v[80:81], v[66:67] neg_lo:[0,1] neg_hi:[0,1]
	s_nop 0
	v_pk_mul_f32 v[80:81], v[50:51], v[66:67] op_sel:[0,1] op_sel_hi:[0,0] neg_lo:[0,1]
	v_pk_fma_f32 v[66:67], v[20:21], v[66:67], v[80:81] op_sel_hi:[0,1,1] neg_lo:[1,0,0] neg_hi:[1,0,0]
	v_pk_add_f32 v[80:81], v[68:69], v[90:91]
	v_pk_add_f32 v[68:69], v[68:69], v[90:91] neg_lo:[0,1] neg_hi:[0,1]
	v_pk_add_f32 v[90:91], v[92:93], v[74:75]
	v_pk_add_f32 v[74:75], v[92:93], v[74:75] neg_lo:[0,1] neg_hi:[0,1]
	s_nop 0
	v_pk_mul_f32 v[92:93], v[10:11], v[74:75] op_sel:[0,1] op_sel_hi:[0,0] neg_lo:[0,1]
	v_pk_fma_f32 v[74:75], v[10:11], v[74:75], v[92:93] op_sel_hi:[0,1,1]
	v_pk_add_f32 v[92:93], v[52:53], v[96:97]
	v_pk_add_f32 v[52:53], v[52:53], v[96:97] neg_lo:[0,1] neg_hi:[0,1]
	s_nop 0
	v_xor_b32_e32 v96, 0x80000000, v53
	v_mov_b32_e32 v97, v52
	v_pk_add_f32 v[52:53], v[88:89], v[94:95]
	v_pk_add_f32 v[88:89], v[88:89], v[94:95] neg_lo:[0,1] neg_hi:[0,1]
	s_nop 0
	v_pk_mul_f32 v[94:95], v[10:11], v[88:89] op_sel:[0,1] op_sel_hi:[0,0] neg_lo:[0,1]
	v_pk_fma_f32 v[88:89], v[10:11], v[88:89], v[94:95] op_sel_hi:[0,1,1] neg_lo:[1,0,0] neg_hi:[1,0,0]
	v_pk_add_f32 v[94:95], v[80:81], v[92:93]
	v_pk_add_f32 v[80:81], v[80:81], v[92:93] neg_lo:[0,1] neg_hi:[0,1]
	v_pk_add_f32 v[92:93], v[90:91], v[52:53]
	v_pk_add_f32 v[52:53], v[90:91], v[52:53] neg_lo:[0,1] neg_hi:[0,1]
	s_nop 0
	v_xor_b32_e32 v90, 0x80000000, v53
	v_mov_b32_e32 v91, v52
	v_pk_add_f32 v[52:53], v[94:95], v[92:93]
	v_pk_add_f32 v[92:93], v[94:95], v[92:93] neg_lo:[0,1] neg_hi:[0,1]
	v_pk_add_f32 v[94:95], v[80:81], v[90:91]
	v_pk_add_f32 v[80:81], v[80:81], v[90:91] neg_lo:[0,1] neg_hi:[0,1]
	v_pk_add_f32 v[90:91], v[68:69], v[96:97]
	v_pk_add_f32 v[68:69], v[68:69], v[96:97] neg_lo:[0,1] neg_hi:[0,1]
	v_pk_add_f32 v[96:97], v[74:75], v[88:89]
	v_pk_add_f32 v[74:75], v[74:75], v[88:89] neg_lo:[0,1] neg_hi:[0,1]
	s_nop 0
	v_xor_b32_e32 v88, 0x80000000, v75
	v_mov_b32_e32 v89, v74
	v_pk_add_f32 v[74:75], v[90:91], v[96:97]
	v_pk_add_f32 v[90:91], v[90:91], v[96:97] neg_lo:[0,1] neg_hi:[0,1]
	v_pk_add_f32 v[96:97], v[68:69], v[88:89]
	v_pk_add_f32 v[68:69], v[68:69], v[88:89] neg_lo:[0,1] neg_hi:[0,1]
	v_pk_add_f32 v[88:89], v[82:83], v[84:85]
	v_pk_add_f32 v[82:83], v[82:83], v[84:85] neg_lo:[0,1] neg_hi:[0,1]
	v_pk_add_f32 v[84:85], v[34:35], v[76:77]
	v_pk_add_f32 v[34:35], v[34:35], v[76:77] neg_lo:[0,1] neg_hi:[0,1]
	s_nop 0
	v_pk_mul_f32 v[76:77], v[10:11], v[34:35] op_sel:[0,1] op_sel_hi:[0,0] neg_lo:[0,1]
	v_pk_fma_f32 v[34:35], v[10:11], v[34:35], v[76:77] op_sel_hi:[0,1,1]
	v_pk_add_f32 v[76:77], v[70:71], v[78:79]
	v_pk_add_f32 v[70:71], v[70:71], v[78:79] neg_lo:[0,1] neg_hi:[0,1]
	s_nop 0
	v_xor_b32_e32 v78, 0x80000000, v71
	v_mov_b32_e32 v79, v70
	v_pk_add_f32 v[70:71], v[72:73], v[66:67]
	v_pk_add_f32 v[66:67], v[72:73], v[66:67] neg_lo:[0,1] neg_hi:[0,1]
	s_nop 0
	v_pk_mul_f32 v[72:73], v[10:11], v[66:67] op_sel:[0,1] op_sel_hi:[0,0] neg_lo:[0,1]
	v_pk_fma_f32 v[66:67], v[10:11], v[66:67], v[72:73] op_sel_hi:[0,1,1] neg_lo:[1,0,0] neg_hi:[1,0,0]
	v_pk_add_f32 v[72:73], v[88:89], v[76:77]
	v_pk_add_f32 v[76:77], v[88:89], v[76:77] neg_lo:[0,1] neg_hi:[0,1]
	v_pk_add_f32 v[88:89], v[84:85], v[70:71]
	v_pk_add_f32 v[70:71], v[84:85], v[70:71] neg_lo:[0,1] neg_hi:[0,1]
	s_nop 0
	v_xor_b32_e32 v84, 0x80000000, v71
	v_mov_b32_e32 v85, v70
	v_pk_add_f32 v[70:71], v[72:73], v[88:89]
	v_pk_add_f32 v[72:73], v[72:73], v[88:89] neg_lo:[0,1] neg_hi:[0,1]
	v_pk_add_f32 v[88:89], v[76:77], v[84:85]
	v_pk_add_f32 v[76:77], v[76:77], v[84:85] neg_lo:[0,1] neg_hi:[0,1]
	v_pk_add_f32 v[84:85], v[82:83], v[78:79]
	v_pk_add_f32 v[78:79], v[82:83], v[78:79] neg_lo:[0,1] neg_hi:[0,1]
	v_pk_add_f32 v[82:83], v[34:35], v[66:67]
	v_pk_add_f32 v[34:35], v[34:35], v[66:67] neg_lo:[0,1] neg_hi:[0,1]
	s_nop 0
	v_xor_b32_e32 v66, 0x80000000, v35
	v_mov_b32_e32 v67, v34
	v_pk_add_f32 v[34:35], v[84:85], v[82:83]
	v_pk_add_f32 v[82:83], v[84:85], v[82:83] neg_lo:[0,1] neg_hi:[0,1]
	v_pk_add_f32 v[84:85], v[78:79], v[66:67]
	v_pk_add_f32 v[66:67], v[78:79], v[66:67] neg_lo:[0,1] neg_hi:[0,1]
	v_pk_add_f32 v[78:79], v[16:17], v[86:87]
	v_pk_add_f32 v[16:17], v[16:17], v[86:87] neg_lo:[0,1] neg_hi:[0,1]
	v_pk_add_f32 v[86:87], v[18:19], v[36:37]
	v_pk_add_f32 v[18:19], v[18:19], v[36:37] neg_lo:[0,1] neg_hi:[0,1]
	s_nop 0
	v_pk_mul_f32 v[36:37], v[50:51], v[18:19] op_sel:[0,1] op_sel_hi:[0,0] neg_lo:[0,1]
	v_pk_fma_f32 v[18:19], v[20:21], v[18:19], v[36:37] op_sel_hi:[0,1,1]
	v_pk_add_f32 v[36:37], v[22:23], v[38:39]
	v_pk_add_f32 v[22:23], v[22:23], v[38:39] neg_lo:[0,1] neg_hi:[0,1]
	s_nop 0
	v_pk_mul_f32 v[38:39], v[10:11], v[22:23] op_sel:[0,1] op_sel_hi:[0,0] neg_lo:[0,1]
	v_pk_fma_f32 v[22:23], v[10:11], v[22:23], v[38:39] op_sel_hi:[0,1,1]
	v_pk_add_f32 v[38:39], v[24:25], v[40:41]
	v_pk_add_f32 v[24:25], v[24:25], v[40:41] neg_lo:[0,1] neg_hi:[0,1]
	s_nop 0
	v_pk_mul_f32 v[40:41], v[20:21], v[24:25] op_sel:[0,1] op_sel_hi:[0,0] neg_lo:[0,1]
	v_pk_fma_f32 v[24:25], v[50:51], v[24:25], v[40:41] op_sel_hi:[0,1,1]
	v_pk_add_f32 v[40:41], v[28:29], v[44:45]
	v_pk_add_f32 v[28:29], v[28:29], v[44:45] neg_lo:[0,1] neg_hi:[0,1]
	s_nop 0
	v_xor_b32_e32 v44, 0x80000000, v29
	v_mov_b32_e32 v45, v28
	v_pk_add_f32 v[28:29], v[26:27], v[42:43]
	v_pk_add_f32 v[26:27], v[26:27], v[42:43] neg_lo:[0,1] neg_hi:[0,1]
	s_nop 0
	v_pk_mul_f32 v[42:43], v[20:21], v[26:27] op_sel:[0,1] op_sel_hi:[0,0] neg_lo:[0,1]
	v_pk_fma_f32 v[26:27], v[50:51], v[26:27], v[42:43] op_sel_hi:[0,1,1] neg_lo:[1,0,0] neg_hi:[1,0,0]
	v_pk_add_f32 v[42:43], v[30:31], v[46:47]
	v_pk_add_f32 v[30:31], v[30:31], v[46:47] neg_lo:[0,1] neg_hi:[0,1]
	s_nop 0
	v_pk_mul_f32 v[46:47], v[10:11], v[30:31] op_sel:[0,1] op_sel_hi:[0,0] neg_lo:[0,1]
	v_pk_fma_f32 v[30:31], v[10:11], v[30:31], v[46:47] op_sel_hi:[0,1,1] neg_lo:[1,0,0] neg_hi:[1,0,0]
	v_pk_add_f32 v[46:47], v[32:33], v[48:49]
	v_pk_add_f32 v[32:33], v[32:33], v[48:49] neg_lo:[0,1] neg_hi:[0,1]
	s_nop 0
	v_pk_mul_f32 v[48:49], v[50:51], v[32:33] op_sel:[0,1] op_sel_hi:[0,0] neg_lo:[0,1]
	v_pk_fma_f32 v[20:21], v[20:21], v[32:33], v[48:49] op_sel_hi:[0,1,1] neg_lo:[1,0,0] neg_hi:[1,0,0]
	v_pk_add_f32 v[48:49], v[86:87], v[28:29]
	v_pk_add_f32 v[28:29], v[86:87], v[28:29] neg_lo:[0,1] neg_hi:[0,1]
	v_pk_add_f32 v[32:33], v[78:79], v[40:41]
	v_pk_add_f32 v[40:41], v[78:79], v[40:41] neg_lo:[0,1] neg_hi:[0,1]
	v_pk_mul_f32 v[78:79], v[10:11], v[28:29] op_sel:[0,1] op_sel_hi:[0,0] neg_lo:[0,1]
	v_pk_fma_f32 v[28:29], v[10:11], v[28:29], v[78:79] op_sel_hi:[0,1,1]
	v_pk_add_f32 v[78:79], v[36:37], v[42:43]
	v_pk_add_f32 v[36:37], v[36:37], v[42:43] neg_lo:[0,1] neg_hi:[0,1]
	s_nop 0
	v_xor_b32_e32 v42, 0x80000000, v37
	v_mov_b32_e32 v43, v36
	v_pk_add_f32 v[36:37], v[38:39], v[46:47]
	v_pk_add_f32 v[38:39], v[38:39], v[46:47] neg_lo:[0,1] neg_hi:[0,1]
	s_nop 0
	v_pk_mul_f32 v[46:47], v[10:11], v[38:39] op_sel:[0,1] op_sel_hi:[0,0] neg_lo:[0,1]
	v_pk_fma_f32 v[38:39], v[10:11], v[38:39], v[46:47] op_sel_hi:[0,1,1] neg_lo:[1,0,0] neg_hi:[1,0,0]
	v_pk_add_f32 v[46:47], v[32:33], v[78:79]
	v_pk_add_f32 v[32:33], v[32:33], v[78:79] neg_lo:[0,1] neg_hi:[0,1]
	v_pk_add_f32 v[78:79], v[48:49], v[36:37]
	v_pk_add_f32 v[36:37], v[48:49], v[36:37] neg_lo:[0,1] neg_hi:[0,1]
	s_nop 0
	v_pk_add_f32 v[86:87], v[32:33], v[36:37] op_sel:[0,1] op_sel_hi:[1,0] neg_lo:[0,1]
	v_pk_add_f32 v[32:33], v[32:33], v[36:37] op_sel:[0,1] op_sel_hi:[1,0] neg_hi:[0,1]
	v_pk_add_f32 v[48:49], v[40:41], v[42:43]
	v_pk_add_f32 v[40:41], v[40:41], v[42:43] neg_lo:[0,1] neg_hi:[0,1]
	v_pk_add_f32 v[42:43], v[28:29], v[38:39]
	v_pk_add_f32 v[28:29], v[28:29], v[38:39] neg_lo:[0,1] neg_hi:[0,1]
	v_pk_add_f32 v[36:37], v[46:47], v[78:79] neg_lo:[0,1] neg_hi:[0,1]
	v_xor_b32_e32 v38, 0x80000000, v29
	v_mov_b32_e32 v39, v28
	v_pk_add_f32 v[28:29], v[48:49], v[42:43]
	v_pk_add_f32 v[42:43], v[48:49], v[42:43] neg_lo:[0,1] neg_hi:[0,1]
	v_pk_add_f32 v[48:49], v[40:41], v[38:39]
	v_pk_add_f32 v[38:39], v[40:41], v[38:39] neg_lo:[0,1] neg_hi:[0,1]
	v_pk_add_f32 v[40:41], v[16:17], v[44:45]
	v_pk_add_f32 v[16:17], v[16:17], v[44:45] neg_lo:[0,1] neg_hi:[0,1]
	v_pk_add_f32 v[44:45], v[18:19], v[26:27]
	v_pk_add_f32 v[18:19], v[18:19], v[26:27] neg_lo:[0,1] neg_hi:[0,1]
	s_nop 0
	v_pk_mul_f32 v[26:27], v[10:11], v[18:19] op_sel:[0,1] op_sel_hi:[0,0] neg_lo:[0,1]
	v_pk_fma_f32 v[18:19], v[10:11], v[18:19], v[26:27] op_sel_hi:[0,1,1]
	v_pk_add_f32 v[26:27], v[22:23], v[30:31]
	v_pk_add_f32 v[22:23], v[22:23], v[30:31] neg_lo:[0,1] neg_hi:[0,1]
	s_nop 0
	v_xor_b32_e32 v30, 0x80000000, v23
	v_mov_b32_e32 v31, v22
	v_pk_add_f32 v[22:23], v[24:25], v[20:21]
	v_pk_add_f32 v[20:21], v[24:25], v[20:21] neg_lo:[0,1] neg_hi:[0,1]
	s_nop 0
	v_pk_mul_f32 v[24:25], v[10:11], v[20:21] op_sel:[0,1] op_sel_hi:[0,0] neg_lo:[0,1]
	v_pk_fma_f32 v[20:21], v[10:11], v[20:21], v[24:25] op_sel_hi:[0,1,1] neg_lo:[1,0,0] neg_hi:[1,0,0]
	v_pk_add_f32 v[24:25], v[40:41], v[26:27]
	v_pk_add_f32 v[26:27], v[40:41], v[26:27] neg_lo:[0,1] neg_hi:[0,1]
	v_pk_add_f32 v[40:41], v[44:45], v[22:23]
	v_pk_add_f32 v[22:23], v[44:45], v[22:23] neg_lo:[0,1] neg_hi:[0,1]
	s_nop 0
	v_xor_b32_e32 v44, 0x80000000, v23
	v_mov_b32_e32 v45, v22
	v_pk_add_f32 v[22:23], v[24:25], v[40:41]
	v_pk_add_f32 v[24:25], v[24:25], v[40:41] neg_lo:[0,1] neg_hi:[0,1]
	v_pk_add_f32 v[40:41], v[26:27], v[44:45]
	v_pk_add_f32 v[26:27], v[26:27], v[44:45] neg_lo:[0,1] neg_hi:[0,1]
	v_pk_add_f32 v[44:45], v[16:17], v[30:31]
	v_pk_add_f32 v[16:17], v[16:17], v[30:31] neg_lo:[0,1] neg_hi:[0,1]
	v_pk_add_f32 v[30:31], v[18:19], v[20:21]
	v_pk_add_f32 v[18:19], v[18:19], v[20:21] neg_lo:[0,1] neg_hi:[0,1]
	s_nop 0
	v_xor_b32_e32 v20, 0x80000000, v19
	v_mov_b32_e32 v21, v18
	v_pk_add_f32 v[18:19], v[44:45], v[30:31]
	v_pk_add_f32 v[30:31], v[44:45], v[30:31] neg_lo:[0,1] neg_hi:[0,1]
	v_pk_add_f32 v[44:45], v[16:17], v[20:21]
	v_pk_add_f32 v[16:17], v[16:17], v[20:21] neg_lo:[0,1] neg_hi:[0,1]
	v_pk_add_f32 v[20:21], v[46:47], v[78:79]
	ds_write2_b64 v13, v[52:53], v[20:21] offset1:16
	ds_write2_b64 v15, v[70:71], v[22:23] offset0:32 offset1:48
	ds_write2_b64 v51, v[74:75], v[28:29] offset0:64 offset1:80
	ds_write2_b64 v54, v[34:35], v[18:19] offset0:96 offset1:112
	ds_write2_b64 v55, v[94:95], v[86:87] offset0:128 offset1:144
	ds_write2_b64 v56, v[88:89], v[40:41] offset0:160 offset1:176
	ds_write2_b64 v57, v[96:97], v[48:49] offset0:192 offset1:208
	ds_write2_b64 v58, v[84:85], v[44:45] offset0:224 offset1:240
	ds_write2_b64 v59, v[92:93], v[36:37] offset1:16
	ds_write2_b64 v60, v[72:73], v[24:25] offset0:32 offset1:48
	ds_write2_b64 v61, v[90:91], v[42:43] offset0:64 offset1:80
	ds_write2_b64 v62, v[82:83], v[30:31] offset0:96 offset1:112
	ds_write2_b64 v63, v[80:81], v[32:33] offset0:128 offset1:144
	ds_write2_b64 v64, v[76:77], v[26:27] offset0:160 offset1:176
	ds_write2_b64 v65, v[68:69], v[38:39] offset0:192 offset1:208
	ds_write2_b64 v101, v[66:67], v[16:17] offset0:224 offset1:240
	v_mov_b32_e32 v10, v173
	s_waitcnt lgkmcnt(0)
	s_barrier
	v_lshl_add_u32 v10, v10, 3, 0
	ds_read_b64 v[16:17], v10
	ds_read_b64 v[80:81], v10 offset:4224
	ds_read_b64 v[78:79], v10 offset:8448
	ds_read_b64 v[76:77], v10 offset:12672
	ds_read_b64 v[74:75], v10 offset:16896
	ds_read_b64 v[72:73], v10 offset:21120
	ds_read_b64 v[70:71], v10 offset:25344
	ds_read_b64 v[68:69], v10 offset:29568
	ds_read_b64 v[24:25], v10 offset:33792
	ds_read_b64 v[62:63], v10 offset:38016
	ds_read_b64 v[60:61], v10 offset:42240
	ds_read_b64 v[58:59], v10 offset:46464
	ds_read_b64 v[54:55], v10 offset:50688
	ds_read_b64 v[50:51], v10 offset:54912
	ds_read_b64 v[46:47], v10 offset:59136
	ds_read_b64 v[44:45], v10 offset:63360
	v_add_u32_e32 v13, 0x10800, v10
	v_add_u32_e32 v15, 0x11880, v10
	v_add_u32_e32 v20, 0x12900, v10
	v_add_u32_e32 v21, 0x13980, v10
	ds_read_b64 v[18:19], v13
	ds_read_b64 v[66:67], v15
	ds_read_b64 v[64:65], v20
	ds_read_b64 v[38:39], v21
	v_add_u32_e32 v13, 0x14a00, v10
	v_add_u32_e32 v15, 0x15a80, v10
	v_add_u32_e32 v20, 0x16b00, v10
	v_add_u32_e32 v21, 0x17b80, v10
	ds_read_b64 v[30:31], v13
	ds_read_b64 v[56:57], v15
	ds_read_b64 v[52:53], v20
	ds_read_b64 v[48:49], v21
	v_add_u32_e32 v13, 0x18c00, v10
	v_add_u32_e32 v15, 0x19c80, v10
	v_add_u32_e32 v20, 0x1ad00, v10
	v_add_u32_e32 v21, 0x1bd80, v10
	ds_read_b64 v[82:83], v13
	ds_read_b64 v[42:43], v15
	ds_read_b64 v[40:41], v20
	ds_read_b64 v[36:37], v21
	v_add_u32_e32 v13, 0x1ce00, v10
	v_add_u32_e32 v15, 0x1de80, v10
	v_add_u32_e32 v20, 0x1ef00, v10
	v_add_u32_e32 v10, 0x1ff80, v10
	ds_read_b64 v[34:35], v13
	ds_read_b64 v[32:33], v15
	ds_read_b64 v[28:29], v20
	ds_read_b64 v[26:27], v10
	v_pk_fma_f32 v[84:85], v[178:179], s[90:91], v[178:179] op_sel:[1,0,0] op_sel_hi:[0,1,1]
	v_pk_mul_f32 v[20:21], v[178:179], v[84:85] op_sel:[1,1] op_sel_hi:[0,1] neg_lo:[0,1]
	v_pk_fma_f32 v[86:87], v[178:179], v[84:85], v[20:21] op_sel_hi:[1,0,1]
	v_pk_mul_f32 v[20:21], v[178:179], v[86:87] op_sel:[1,1] op_sel_hi:[0,1] neg_lo:[0,1]
	v_pk_fma_f32 v[88:89], v[178:179], v[86:87], v[20:21] op_sel_hi:[1,0,1]
	v_pk_mul_f32 v[20:21], v[178:179], v[88:89] op_sel:[1,1] op_sel_hi:[0,1] neg_lo:[0,1]
	v_pk_fma_f32 v[90:91], v[178:179], v[88:89], v[20:21] op_sel_hi:[1,0,1]
	v_mov_b32_e32 v10, v164
	v_pk_mul_f32 v[20:21], v[178:179], v[90:91] op_sel:[1,1] op_sel_hi:[0,1] neg_lo:[0,1]
	v_pk_fma_f32 v[92:93], v[178:179], v[90:91], v[20:21] op_sel_hi:[1,0,1]
	s_waitcnt lgkmcnt(14)
	v_fmac_f32_e32 v16, 0, v17
	v_pk_mul_f32 v[20:21], v[178:179], v[92:93] op_sel:[1,1] op_sel_hi:[0,1] neg_lo:[0,1]
	v_pk_fma_f32 v[94:95], v[178:179], v[92:93], v[20:21] op_sel_hi:[1,0,1]
	v_readlane_b32 s70, v251, 22
	v_pk_mul_f32 v[20:21], v[178:179], v[94:95] op_sel:[1,1] op_sel_hi:[0,1] neg_lo:[0,1]
	v_pk_fma_f32 v[96:97], v[178:179], v[94:95], v[20:21] op_sel_hi:[1,0,1]
	v_readlane_b32 s71, v251, 23
	v_pk_mul_f32 v[20:21], v[178:179], v[96:97] op_sel:[1,1] op_sel_hi:[0,1] neg_lo:[0,1]
	v_pk_fma_f32 v[98:99], v[178:179], v[96:97], v[20:21] op_sel_hi:[1,0,1]
	s_movk_i32 s10, 0x1000
	v_pk_mul_f32 v[20:21], v[178:179], v[98:99] op_sel:[1,1] op_sel_hi:[0,1] neg_lo:[0,1]
	v_pk_fma_f32 v[100:101], v[178:179], v[98:99], v[20:21] op_sel_hi:[1,0,1]
	s_movk_i32 s11, 0x2000
	v_pk_mul_f32 v[20:21], v[178:179], v[100:101] op_sel:[1,1] op_sel_hi:[0,1] neg_lo:[0,1]
	v_pk_fma_f32 v[102:103], v[178:179], v[100:101], v[20:21] op_sel_hi:[1,0,1]
	s_movk_i32 s13, 0x5000
	v_pk_mul_f32 v[20:21], v[178:179], v[102:103] op_sel:[1,1] op_sel_hi:[0,1] neg_lo:[0,1]
	v_pk_fma_f32 v[104:105], v[178:179], v[102:103], v[20:21] op_sel_hi:[1,0,1]
	s_movk_i32 s12, 0x6000
	v_pk_mul_f32 v[20:21], v[178:179], v[104:105] op_sel:[1,1] op_sel_hi:[0,1] neg_lo:[0,1]
	v_pk_fma_f32 v[106:107], v[178:179], v[104:105], v[20:21] op_sel_hi:[1,0,1]
	s_movk_i32 s16, 0x7000
	v_pk_mul_f32 v[20:21], v[178:179], v[106:107] op_sel:[1,1] op_sel_hi:[0,1] neg_lo:[0,1]
	v_pk_fma_f32 v[108:109], v[178:179], v[106:107], v[20:21] op_sel_hi:[1,0,1]
	s_mov_b32 s80, 0x3f74fa0b
	v_pk_mul_f32 v[20:21], v[178:179], v[108:109] op_sel:[1,1] op_sel_hi:[0,1] neg_lo:[0,1]
	v_pk_fma_f32 v[110:111], v[178:179], v[108:109], v[20:21] op_sel_hi:[1,0,1]
	s_mov_b32 s81, 0xbe94a031
	v_pk_mul_f32 v[20:21], v[178:179], v[110:111] op_sel:[1,1] op_sel_hi:[0,1] neg_lo:[0,1]
	v_pk_fma_f32 v[112:113], v[178:179], v[110:111], v[20:21] op_sel_hi:[1,0,1]
	s_mov_b32 s20, 0x3f61c598
	v_pk_mul_f32 v[20:21], v[178:179], v[112:113] op_sel:[1,1] op_sel_hi:[0,1] neg_lo:[0,1]
	v_pk_fma_f32 v[20:21], v[178:179], v[112:113], v[20:21] op_sel_hi:[1,0,1]
	s_mov_b32 s21, 0xbef15aea
	v_pk_mul_f32 v[114:115], v[178:179], v[20:21] op_sel:[1,1] op_sel_hi:[0,1] neg_lo:[0,1]
	v_pk_fma_f32 v[114:115], v[178:179], v[20:21], v[114:115] op_sel_hi:[1,0,1]
	v_mul_f32_e32 v18, v18, v20
	v_pk_mul_f32 v[116:117], v[178:179], v[114:115] op_sel:[1,1] op_sel_hi:[0,1] neg_lo:[0,1]
	v_pk_fma_f32 v[116:117], v[178:179], v[114:115], v[116:117] op_sel_hi:[1,0,1]
	v_fmac_f32_e32 v18, v19, v21
	v_pk_mul_f32 v[118:119], v[178:179], v[116:117] op_sel:[1,1] op_sel_hi:[0,1] neg_lo:[0,1]
	v_pk_fma_f32 v[118:119], v[178:179], v[116:117], v[118:119] op_sel_hi:[1,0,1]
	v_add_f32_e32 v17, v16, v18
	v_pk_mul_f32 v[120:121], v[178:179], v[118:119] op_sel:[1,1] op_sel_hi:[0,1] neg_lo:[0,1]
	v_pk_fma_f32 v[120:121], v[178:179], v[118:119], v[120:121] op_sel_hi:[1,0,1]
	s_mov_b32 s40, s45
	v_pk_mul_f32 v[122:123], v[178:179], v[120:121] op_sel:[1,1] op_sel_hi:[0,1] neg_lo:[0,1]
	v_pk_fma_f32 v[122:123], v[178:179], v[120:121], v[122:123] op_sel_hi:[1,0,1]
	s_mov_b32 s41, s94
	v_pk_mul_f32 v[124:125], v[178:179], v[122:123] op_sel:[1,1] op_sel_hi:[0,1] neg_lo:[0,1]
	v_pk_fma_f32 v[124:125], v[178:179], v[122:123], v[124:125] op_sel_hi:[1,0,1]
	s_mov_b32 s86, 0x3f226799
	v_pk_mul_f32 v[126:127], v[178:179], v[124:125] op_sel:[1,1] op_sel_hi:[0,1] neg_lo:[0,1]
	v_pk_fma_f32 v[126:127], v[178:179], v[124:125], v[126:127] op_sel_hi:[1,0,1]
	s_mov_b32 s87, 0xbf45e403
	v_pk_mul_f32 v[128:129], v[178:179], v[126:127] op_sel:[1,1] op_sel_hi:[0,1] neg_lo:[0,1]
	v_pk_fma_f32 v[128:129], v[178:179], v[126:127], v[128:129] op_sel_hi:[1,0,1]
	s_mov_b32 s24, 0x3f0e39da
	v_pk_mul_f32 v[130:131], v[178:179], v[128:129] op_sel:[1,1] op_sel_hi:[0,1] neg_lo:[0,1]
	v_pk_fma_f32 v[130:131], v[178:179], v[128:129], v[130:131] op_sel_hi:[1,0,1]
	s_mov_b32 s25, 0xbf54db31
	v_pk_mul_f32 v[132:133], v[178:179], v[130:131] op_sel:[1,1] op_sel_hi:[0,1] neg_lo:[0,1]
	v_pk_fma_f32 v[132:133], v[178:179], v[130:131], v[132:133] op_sel_hi:[1,0,1]
	s_mov_b32 s88, 0x3ef15aea
	v_pk_mul_f32 v[134:135], v[178:179], v[132:133] op_sel:[1,1] op_sel_hi:[0,1] neg_lo:[0,1]
	v_pk_fma_f32 v[134:135], v[178:179], v[132:133], v[134:135] op_sel_hi:[1,0,1]
	s_mov_b32 s89, 0xbf61c598
	v_pk_mul_f32 v[136:137], v[178:179], v[134:135] op_sel:[1,1] op_sel_hi:[0,1] neg_lo:[0,1]
	v_pk_fma_f32 v[136:137], v[178:179], v[134:135], v[136:137] op_sel_hi:[1,0,1]
	s_mov_b32 s18, 0x3ec3ef15
	v_pk_mul_f32 v[138:139], v[178:179], v[136:137] op_sel:[1,1] op_sel_hi:[0,1] neg_lo:[0,1]
	v_pk_fma_f32 v[138:139], v[178:179], v[136:137], v[138:139] op_sel_hi:[1,0,1]
	s_mov_b32 s19, 0xbf6c835e
	v_pk_mul_f32 v[140:141], v[178:179], v[138:139] op_sel:[1,1] op_sel_hi:[0,1] neg_lo:[0,1]
	v_pk_fma_f32 v[140:141], v[178:179], v[138:139], v[140:141] op_sel_hi:[1,0,1]
	s_mov_b32 s92, 0x3e94a031
	v_pk_mul_f32 v[142:143], v[178:179], v[140:141] op_sel:[1,1] op_sel_hi:[0,1] neg_lo:[0,1]
	v_pk_fma_f32 v[22:23], v[178:179], v[140:141], v[142:143] op_sel_hi:[1,0,1]
	s_waitcnt lgkmcnt(0)
	v_pk_mul_f32 v[142:143], v[26:27], v[22:23] op_sel:[1,1] op_sel_hi:[0,1] neg_hi:[1,0]
	s_mov_b32 s93, 0xbf74fa0b
	v_pk_fma_f32 v[26:27], v[26:27], v[22:23], v[142:143] op_sel_hi:[1,0,1]
	v_pk_mul_f32 v[22:23], v[28:29], v[140:141] op_sel:[1,1] op_sel_hi:[0,1] neg_hi:[1,0]
	s_mov_b32 s82, 0x3f54db31
	v_pk_fma_f32 v[28:29], v[28:29], v[140:141], v[22:23] op_sel_hi:[1,0,1]
	v_pk_mul_f32 v[22:23], v[32:33], v[138:139] op_sel:[1,1] op_sel_hi:[0,1] neg_hi:[1,0]
	s_mov_b32 s83, 0xbf0e39da
	v_pk_fma_f32 v[32:33], v[32:33], v[138:139], v[22:23] op_sel_hi:[1,0,1]
	v_pk_mul_f32 v[22:23], v[34:35], v[136:137] op_sel:[1,1] op_sel_hi:[0,1] neg_hi:[1,0]
	s_mov_b32 s28, 0x3f45e403
	v_pk_fma_f32 v[34:35], v[34:35], v[136:137], v[22:23] op_sel_hi:[1,0,1]
	v_pk_mul_f32 v[22:23], v[36:37], v[134:135] op_sel:[1,1] op_sel_hi:[0,1] neg_hi:[1,0]
	s_mov_b32 s29, 0xbf226799
	v_pk_fma_f32 v[36:37], v[36:37], v[134:135], v[22:23] op_sel_hi:[1,0,1]
	v_pk_mul_f32 v[22:23], v[40:41], v[132:133] op_sel:[1,1] op_sel_hi:[0,1] neg_hi:[1,0]
	s_mov_b32 s36, s97
	v_pk_fma_f32 v[40:41], v[40:41], v[132:133], v[22:23] op_sel_hi:[1,0,1]
	v_pk_mul_f32 v[22:23], v[42:43], v[130:131] op_sel:[1,1] op_sel_hi:[0,1] neg_hi:[1,0]
	s_mov_b32 s37, s95
	v_pk_fma_f32 v[42:43], v[42:43], v[130:131], v[22:23] op_sel_hi:[1,0,1]
	v_pk_mul_f32 v[22:23], v[82:83], v[128:129] op_sel:[1,1] op_sel_hi:[0,1] neg_hi:[1,0]
	s_mov_b32 s96, s95
	v_pk_fma_f32 v[22:23], v[82:83], v[128:129], v[22:23] op_sel_hi:[1,0,1]
	v_pk_mul_f32 v[82:83], v[48:49], v[126:127] op_sel:[1,1] op_sel_hi:[0,1] neg_hi:[1,0]
	s_mov_b32 s23, s25
	v_pk_fma_f32 v[48:49], v[48:49], v[126:127], v[82:83] op_sel_hi:[1,0,1]
	v_pk_mul_f32 v[82:83], v[52:53], v[124:125] op_sel:[1,1] op_sel_hi:[0,1] neg_hi:[1,0]
	s_mov_b32 s22, s83
	v_pk_fma_f32 v[52:53], v[52:53], v[124:125], v[82:83] op_sel_hi:[1,0,1]
	v_pk_mul_f32 v[82:83], v[56:57], v[122:123] op_sel:[1,1] op_sel_hi:[0,1] neg_hi:[1,0]
	s_mov_b32 s26, s29
	v_pk_fma_f32 v[56:57], v[56:57], v[122:123], v[82:83] op_sel_hi:[1,0,1]
	v_pk_mul_f32 v[82:83], v[30:31], v[120:121] op_sel:[1,1] op_sel_hi:[0,1] neg_hi:[1,0]
	s_mov_b32 s27, s87
	v_pk_fma_f32 v[30:31], v[30:31], v[120:121], v[82:83] op_sel_hi:[1,0,1]
	v_pk_mul_f32 v[82:83], v[38:39], v[118:119] op_sel:[1,1] op_sel_hi:[0,1] neg_hi:[1,0]
	s_movk_i32 s39, 0x2000
	v_pk_fma_f32 v[38:39], v[38:39], v[118:119], v[82:83] op_sel_hi:[1,0,1]
	v_pk_mul_f32 v[82:83], v[64:65], v[116:117] op_sel:[1,1] op_sel_hi:[0,1] neg_hi:[1,0]
	s_mov_b32 s44, s94
	v_pk_fma_f32 v[64:65], v[64:65], v[116:117], v[82:83] op_sel_hi:[1,0,1]
	v_pk_mul_f32 v[82:83], v[66:67], v[114:115] op_sel:[1,1] op_sel_hi:[0,1] neg_hi:[1,0]
	v_mov_b32_e32 v118, v164
	v_pk_fma_f32 v[66:67], v[66:67], v[114:115], v[82:83] op_sel_hi:[1,0,1]
	v_pk_mul_f32 v[82:83], v[44:45], v[112:113] op_sel:[1,1] op_sel_hi:[0,1] neg_hi:[1,0]
	v_mov_b32_e32 v120, v166
	v_pk_fma_f32 v[44:45], v[44:45], v[112:113], v[82:83] op_sel_hi:[1,0,1]
	v_pk_mul_f32 v[82:83], v[46:47], v[110:111] op_sel:[1,1] op_sel_hi:[0,1] neg_hi:[1,0]
	v_mov_b32_e32 v122, v168
	v_pk_fma_f32 v[46:47], v[46:47], v[110:111], v[82:83] op_sel_hi:[1,0,1]
	v_pk_mul_f32 v[82:83], v[50:51], v[108:109] op_sel:[1,1] op_sel_hi:[0,1] neg_hi:[1,0]
	v_mov_b32_e32 v124, v170
	v_pk_fma_f32 v[50:51], v[50:51], v[108:109], v[82:83] op_sel_hi:[1,0,1]
	v_pk_mul_f32 v[82:83], v[54:55], v[106:107] op_sel:[1,1] op_sel_hi:[0,1] neg_hi:[1,0]
	s_movk_i32 s33, 0x5000
	v_pk_fma_f32 v[54:55], v[54:55], v[106:107], v[82:83] op_sel_hi:[1,0,1]
	v_pk_mul_f32 v[82:83], v[58:59], v[104:105] op_sel:[1,1] op_sel_hi:[0,1] neg_hi:[1,0]
	s_nop 0
	v_pk_fma_f32 v[58:59], v[58:59], v[104:105], v[82:83] op_sel_hi:[1,0,1]
	v_pk_mul_f32 v[82:83], v[60:61], v[102:103] op_sel:[1,1] op_sel_hi:[0,1] neg_hi:[1,0]
	s_nop 0
	v_pk_fma_f32 v[60:61], v[60:61], v[102:103], v[82:83] op_sel_hi:[1,0,1]
	v_pk_mul_f32 v[82:83], v[62:63], v[100:101] op_sel:[1,1] op_sel_hi:[0,1] neg_hi:[1,0]
	s_nop 0
	v_pk_fma_f32 v[62:63], v[62:63], v[100:101], v[82:83] op_sel_hi:[1,0,1]
	v_pk_mul_f32 v[82:83], v[24:25], v[98:99] op_sel:[1,1] op_sel_hi:[0,1] neg_hi:[1,0]
	s_nop 0
	v_pk_fma_f32 v[24:25], v[24:25], v[98:99], v[82:83] op_sel_hi:[1,0,1]
	v_pk_mul_f32 v[82:83], v[68:69], v[96:97] op_sel:[1,1] op_sel_hi:[0,1] neg_hi:[1,0]
	v_add_f32_e32 v22, v24, v22
	v_pk_fma_f32 v[68:69], v[68:69], v[96:97], v[82:83] op_sel_hi:[1,0,1]
	v_pk_mul_f32 v[82:83], v[70:71], v[94:95] op_sel:[1,1] op_sel_hi:[0,1] neg_hi:[1,0]
	v_add_f32_e32 v20, v17, v22
	v_pk_fma_f32 v[70:71], v[70:71], v[94:95], v[82:83] op_sel_hi:[1,0,1]
	v_pk_mul_f32 v[82:83], v[72:73], v[92:93] op_sel:[1,1] op_sel_hi:[0,1] neg_hi:[1,0]
	v_mov_b32_e32 v94, v170
	v_pk_fma_f32 v[72:73], v[72:73], v[92:93], v[82:83] op_sel_hi:[1,0,1]
	v_pk_mul_f32 v[82:83], v[74:75], v[90:91] op_sel:[1,1] op_sel_hi:[0,1] neg_hi:[1,0]
	v_mov_b32_e32 v92, v169
	v_pk_fma_f32 v[74:75], v[74:75], v[90:91], v[82:83] op_sel_hi:[1,0,1]
	v_pk_mul_f32 v[82:83], v[76:77], v[88:89] op_sel:[1,1] op_sel_hi:[0,1] neg_hi:[1,0]
	v_mov_b32_e32 v90, v168
	v_pk_fma_f32 v[76:77], v[76:77], v[88:89], v[82:83] op_sel_hi:[1,0,1]
	v_pk_mul_f32 v[82:83], v[78:79], v[86:87] op_sel:[1,1] op_sel_hi:[0,1] neg_hi:[1,0]
	v_mov_b32_e32 v88, v167
	v_pk_fma_f32 v[78:79], v[78:79], v[86:87], v[82:83] op_sel_hi:[1,0,1]
	v_pk_mul_f32 v[82:83], v[84:85], v[80:81] op_sel:[1,1] op_sel_hi:[1,0] neg_hi:[0,1]
	v_mov_b32_e32 v86, v166
	v_pk_fma_f32 v[80:81], v[80:81], v[84:85], v[82:83] op_sel_hi:[1,0,1]
	v_mov_b32_e32 v84, v165
	v_pk_add_f32 v[96:97], v[80:81], v[66:67]
	v_pk_add_f32 v[66:67], v[80:81], v[66:67] neg_lo:[0,1] neg_hi:[0,1]
	s_nop 0
	v_sub_f32_e32 v82, v25, v23
	v_pk_mul_f32 v[80:81], v[94:95], v[66:67] op_sel:[0,1] op_sel_hi:[0,0] neg_lo:[0,1]
	v_pk_fma_f32 v[80:81], v[10:11], v[66:67], v[80:81] op_sel_hi:[0,1,1]
	v_pk_add_f32 v[66:67], v[78:79], v[64:65]
	v_pk_add_f32 v[64:65], v[78:79], v[64:65] neg_lo:[0,1] neg_hi:[0,1]
	s_nop 0
	v_pk_mul_f32 v[78:79], v[92:93], v[64:65] op_sel:[0,1] op_sel_hi:[0,0] neg_lo:[0,1]
	v_pk_fma_f32 v[64:65], v[84:85], v[64:65], v[78:79] op_sel_hi:[0,1,1]
	v_pk_add_f32 v[78:79], v[76:77], v[38:39]
	v_pk_add_f32 v[38:39], v[76:77], v[38:39] neg_lo:[0,1] neg_hi:[0,1]
	s_barrier
	v_pk_mul_f32 v[76:77], v[90:91], v[38:39] op_sel:[0,1] op_sel_hi:[0,0] neg_lo:[0,1]
	v_pk_fma_f32 v[76:77], v[86:87], v[38:39], v[76:77] op_sel_hi:[0,1,1]
	v_pk_add_f32 v[38:39], v[74:75], v[30:31]
	v_pk_add_f32 v[30:31], v[74:75], v[30:31] neg_lo:[0,1] neg_hi:[0,1]
	s_nop 0
	v_pk_mul_f32 v[74:75], v[88:89], v[30:31] op_sel:[0,1] op_sel_hi:[0,0] neg_lo:[0,1]
	v_pk_fma_f32 v[30:31], v[88:89], v[30:31], v[74:75] op_sel_hi:[0,1,1]
	v_pk_add_f32 v[74:75], v[72:73], v[56:57]
	v_pk_add_f32 v[56:57], v[72:73], v[56:57] neg_lo:[0,1] neg_hi:[0,1]
	v_sub_f32_e32 v22, v17, v22
	v_pk_mul_f32 v[72:73], v[86:87], v[56:57] op_sel:[0,1] op_sel_hi:[0,0] neg_lo:[0,1]
	v_pk_fma_f32 v[72:73], v[90:91], v[56:57], v[72:73] op_sel_hi:[0,1,1]
	v_pk_add_f32 v[56:57], v[70:71], v[52:53]
	v_pk_add_f32 v[52:53], v[70:71], v[52:53] neg_lo:[0,1] neg_hi:[0,1]
	v_ashrrev_i32_e32 v15, 31, v14
	v_pk_mul_f32 v[70:71], v[84:85], v[52:53] op_sel:[0,1] op_sel_hi:[0,0] neg_lo:[0,1]
	v_pk_fma_f32 v[52:53], v[92:93], v[52:53], v[70:71] op_sel_hi:[0,1,1]
	v_pk_add_f32 v[70:71], v[68:69], v[48:49]
	v_pk_add_f32 v[48:49], v[68:69], v[48:49] neg_lo:[0,1] neg_hi:[0,1]
	v_lshl_add_u64 v[14:15], v[14:15], 2, s[70:71]
	v_pk_mul_f32 v[68:69], v[10:11], v[48:49] op_sel:[0,1] op_sel_hi:[0,0] neg_lo:[0,1]
	v_pk_fma_f32 v[98:99], v[94:95], v[48:49], v[68:69] op_sel_hi:[0,1,1]
	v_pk_add_f32 v[48:49], v[62:63], v[42:43]
	v_pk_add_f32 v[42:43], v[62:63], v[42:43] neg_lo:[0,1] neg_hi:[0,1]
	s_nop 0
	v_pk_mul_f32 v[62:63], v[10:11], v[42:43] op_sel:[0,1] op_sel_hi:[0,0] neg_lo:[0,1]
	v_pk_fma_f32 v[62:63], v[94:95], v[42:43], v[62:63] op_sel_hi:[0,1,1] neg_lo:[1,0,0] neg_hi:[1,0,0]
	v_pk_add_f32 v[42:43], v[60:61], v[40:41]
	v_pk_add_f32 v[40:41], v[60:61], v[40:41] neg_lo:[0,1] neg_hi:[0,1]
	s_nop 0
	v_pk_mul_f32 v[60:61], v[84:85], v[40:41] op_sel:[0,1] op_sel_hi:[0,0] neg_lo:[0,1]
	v_pk_fma_f32 v[100:101], v[92:93], v[40:41], v[60:61] op_sel_hi:[0,1,1] neg_lo:[1,0,0] neg_hi:[1,0,0]
	v_pk_add_f32 v[60:61], v[58:59], v[36:37]
	v_pk_add_f32 v[36:37], v[58:59], v[36:37] neg_lo:[0,1] neg_hi:[0,1]
	s_nop 0
	v_pk_mul_f32 v[40:41], v[86:87], v[36:37] op_sel:[0,1] op_sel_hi:[0,0] neg_lo:[0,1]
	v_pk_fma_f32 v[58:59], v[90:91], v[36:37], v[40:41] op_sel_hi:[0,1,1] neg_lo:[1,0,0] neg_hi:[1,0,0]
	v_pk_add_f32 v[40:41], v[54:55], v[34:35]
	v_pk_add_f32 v[34:35], v[54:55], v[34:35] neg_lo:[0,1] neg_hi:[0,1]
	v_pk_add_f32 v[54:55], v[46:47], v[28:29]
	v_pk_mul_f32 v[36:37], v[88:89], v[34:35] op_sel:[0,1] op_sel_hi:[0,0] neg_lo:[0,1]
	v_pk_fma_f32 v[34:35], v[88:89], v[34:35], v[36:37] op_sel_hi:[0,1,1] neg_lo:[1,0,0] neg_hi:[1,0,0]
	v_pk_add_f32 v[36:37], v[50:51], v[32:33]
	v_pk_add_f32 v[32:33], v[50:51], v[32:33] neg_lo:[0,1] neg_hi:[0,1]
	v_pk_add_f32 v[28:29], v[46:47], v[28:29] neg_lo:[0,1] neg_hi:[0,1]
	v_pk_mul_f32 v[50:51], v[90:91], v[32:33] op_sel:[0,1] op_sel_hi:[0,0] neg_lo:[0,1]
	v_pk_fma_f32 v[86:87], v[86:87], v[32:33], v[50:51] op_sel_hi:[0,1,1] neg_lo:[1,0,0] neg_hi:[1,0,0]
	v_pk_mul_f32 v[32:33], v[92:93], v[28:29] op_sel:[0,1] op_sel_hi:[0,0] neg_lo:[0,1]
	v_pk_fma_f32 v[46:47], v[84:85], v[28:29], v[32:33] op_sel_hi:[0,1,1] neg_lo:[1,0,0] neg_hi:[1,0,0]
	v_pk_add_f32 v[28:29], v[44:45], v[26:27]
	v_pk_add_f32 v[26:27], v[44:45], v[26:27] neg_lo:[0,1] neg_hi:[0,1]
	v_pk_add_f32 v[50:51], v[66:67], v[42:43]
	v_pk_mul_f32 v[32:33], v[94:95], v[26:27] op_sel:[0,1] op_sel_hi:[0,0] neg_lo:[0,1]
	v_pk_fma_f32 v[90:91], v[10:11], v[26:27], v[32:33] op_sel_hi:[0,1,1] neg_lo:[1,0,0] neg_hi:[1,0,0]
	v_pk_add_f32 v[32:33], v[96:97], v[48:49] neg_lo:[0,1] neg_hi:[0,1]
	v_pk_add_f32 v[26:27], v[96:97], v[48:49]
	v_pk_mul_f32 v[44:45], v[92:93], v[32:33] op_sel:[0,1] op_sel_hi:[0,0] neg_lo:[0,1]
	v_pk_fma_f32 v[48:49], v[84:85], v[32:33], v[44:45] op_sel_hi:[0,1,1]
	v_pk_add_f32 v[32:33], v[66:67], v[42:43] neg_lo:[0,1] neg_hi:[0,1]
	v_pk_add_f32 v[44:45], v[78:79], v[60:61] neg_lo:[0,1] neg_hi:[0,1]
	v_pk_mul_f32 v[42:43], v[88:89], v[32:33] op_sel:[0,1] op_sel_hi:[0,0] neg_lo:[0,1]
	v_pk_fma_f32 v[32:33], v[88:89], v[32:33], v[42:43] op_sel_hi:[0,1,1]
	v_pk_add_f32 v[42:43], v[78:79], v[60:61]
	v_pk_mul_f32 v[60:61], v[84:85], v[44:45] op_sel:[0,1] op_sel_hi:[0,0] neg_lo:[0,1]
	v_pk_add_f32 v[78:79], v[74:75], v[36:37]
	v_pk_add_f32 v[36:37], v[74:75], v[36:37] neg_lo:[0,1] neg_hi:[0,1]
	v_pk_fma_f32 v[68:69], v[92:93], v[44:45], v[60:61] op_sel_hi:[0,1,1]
	v_pk_mul_f32 v[44:45], v[84:85], v[36:37] op_sel:[0,1] op_sel_hi:[0,0] neg_lo:[0,1]
	v_pk_fma_f32 v[74:75], v[92:93], v[36:37], v[44:45] op_sel_hi:[0,1,1] neg_lo:[1,0,0] neg_hi:[1,0,0]
	v_pk_add_f32 v[36:37], v[56:57], v[54:55] neg_lo:[0,1] neg_hi:[0,1]
	v_pk_add_f32 v[60:61], v[56:57], v[54:55]
	v_pk_mul_f32 v[44:45], v[88:89], v[36:37] op_sel:[0,1] op_sel_hi:[0,0] neg_lo:[0,1]
	v_pk_fma_f32 v[44:45], v[88:89], v[36:37], v[44:45] op_sel_hi:[0,1,1] neg_lo:[1,0,0] neg_hi:[1,0,0]
	v_pk_add_f32 v[36:37], v[70:71], v[28:29]
	v_pk_add_f32 v[28:29], v[70:71], v[28:29] neg_lo:[0,1] neg_hi:[0,1]
	v_pk_add_f32 v[66:67], v[26:27], v[78:79]
	v_pk_mul_f32 v[54:55], v[92:93], v[28:29] op_sel:[0,1] op_sel_hi:[0,0] neg_lo:[0,1]
	v_pk_add_f32 v[26:27], v[26:27], v[78:79] neg_lo:[0,1] neg_hi:[0,1]
	v_pk_fma_f32 v[94:95], v[84:85], v[28:29], v[54:55] op_sel_hi:[0,1,1] neg_lo:[1,0,0] neg_hi:[1,0,0]
	v_pk_mul_f32 v[28:29], v[88:89], v[26:27] op_sel:[0,1] op_sel_hi:[0,0] neg_lo:[0,1]
	v_pk_fma_f32 v[26:27], v[88:89], v[26:27], v[28:29] op_sel_hi:[0,1,1]
	v_pk_add_f32 v[28:29], v[42:43], v[36:37] neg_lo:[0,1] neg_hi:[0,1]
	v_pk_add_f32 v[70:71], v[42:43], v[36:37]
	v_pk_mul_f32 v[36:37], v[88:89], v[28:29] op_sel:[0,1] op_sel_hi:[0,0] neg_lo:[0,1]
	v_pk_fma_f32 v[36:37], v[88:89], v[28:29], v[36:37] op_sel_hi:[0,1,1] neg_lo:[1,0,0] neg_hi:[1,0,0]
	v_pk_add_f32 v[28:29], v[48:49], v[74:75] neg_lo:[0,1] neg_hi:[0,1]
	v_pk_add_f32 v[54:55], v[48:49], v[74:75]
	v_pk_mul_f32 v[42:43], v[88:89], v[28:29] op_sel:[0,1] op_sel_hi:[0,0] neg_lo:[0,1]
	v_pk_fma_f32 v[28:29], v[88:89], v[28:29], v[42:43] op_sel_hi:[0,1,1]
	v_pk_add_f32 v[42:43], v[68:69], v[94:95] neg_lo:[0,1] neg_hi:[0,1]
	v_pk_add_f32 v[74:75], v[80:81], v[62:63]
	v_pk_mul_f32 v[48:49], v[88:89], v[42:43] op_sel:[0,1] op_sel_hi:[0,0] neg_lo:[0,1]
	v_pk_fma_f32 v[42:43], v[88:89], v[42:43], v[48:49] op_sel_hi:[0,1,1] neg_lo:[1,0,0] neg_hi:[1,0,0]
	v_pk_add_f32 v[48:49], v[80:81], v[62:63] neg_lo:[0,1] neg_hi:[0,1]
	v_pk_add_f32 v[56:57], v[68:69], v[94:95]
	v_pk_mul_f32 v[62:63], v[92:93], v[48:49] op_sel:[0,1] op_sel_hi:[0,0] neg_lo:[0,1]
	v_pk_fma_f32 v[94:95], v[84:85], v[48:49], v[62:63] op_sel_hi:[0,1,1]
	v_pk_add_f32 v[48:49], v[64:65], v[100:101] neg_lo:[0,1] neg_hi:[0,1]
	v_pk_add_f32 v[68:69], v[64:65], v[100:101]
	v_pk_mul_f32 v[62:63], v[88:89], v[48:49] op_sel:[0,1] op_sel_hi:[0,0] neg_lo:[0,1]
	v_pk_add_f32 v[64:65], v[76:77], v[58:59]
	v_pk_add_f32 v[58:59], v[76:77], v[58:59] neg_lo:[0,1] neg_hi:[0,1]
	v_pk_fma_f32 v[48:49], v[88:89], v[48:49], v[62:63] op_sel_hi:[0,1,1]
	v_pk_mul_f32 v[62:63], v[84:85], v[58:59] op_sel:[0,1] op_sel_hi:[0,0] neg_lo:[0,1]
	v_pk_fma_f32 v[96:97], v[92:93], v[58:59], v[62:63] op_sel_hi:[0,1,1]
	v_pk_add_f32 v[58:59], v[72:73], v[86:87] neg_lo:[0,1] neg_hi:[0,1]
	v_pk_add_f32 v[76:77], v[52:53], v[46:47]
	v_pk_add_f32 v[46:47], v[52:53], v[46:47] neg_lo:[0,1] neg_hi:[0,1]
	v_pk_add_f32 v[62:63], v[72:73], v[86:87]
	v_pk_mul_f32 v[72:73], v[84:85], v[58:59] op_sel:[0,1] op_sel_hi:[0,0] neg_lo:[0,1]
	v_pk_mul_f32 v[52:53], v[88:89], v[46:47] op_sel:[0,1] op_sel_hi:[0,0] neg_lo:[0,1]
	v_pk_fma_f32 v[86:87], v[92:93], v[58:59], v[72:73] op_sel_hi:[0,1,1] neg_lo:[1,0,0] neg_hi:[1,0,0]
	v_pk_fma_f32 v[58:59], v[88:89], v[46:47], v[52:53] op_sel_hi:[0,1,1] neg_lo:[1,0,0] neg_hi:[1,0,0]
	v_pk_add_f32 v[46:47], v[98:99], v[90:91]
	v_pk_add_f32 v[52:53], v[98:99], v[90:91] neg_lo:[0,1] neg_hi:[0,1]
	v_pk_add_f32 v[80:81], v[64:65], v[46:47]
	v_pk_add_f32 v[46:47], v[64:65], v[46:47] neg_lo:[0,1] neg_hi:[0,1]
	s_nop 0
	v_pk_mul_f32 v[64:65], v[88:89], v[46:47] op_sel:[0,1] op_sel_hi:[0,0] neg_lo:[0,1]
	v_pk_fma_f32 v[64:65], v[88:89], v[46:47], v[64:65] op_sel_hi:[0,1,1] neg_lo:[1,0,0] neg_hi:[1,0,0]
	v_pk_add_f32 v[46:47], v[94:95], v[86:87] neg_lo:[0,1] neg_hi:[0,1]
	v_pk_mul_f32 v[72:73], v[92:93], v[52:53] op_sel:[0,1] op_sel_hi:[0,0] neg_lo:[0,1]
	v_pk_add_f32 v[78:79], v[74:75], v[62:63]
	v_pk_add_f32 v[62:63], v[74:75], v[62:63] neg_lo:[0,1] neg_hi:[0,1]
	v_pk_fma_f32 v[52:53], v[84:85], v[52:53], v[72:73] op_sel_hi:[0,1,1] neg_lo:[1,0,0] neg_hi:[1,0,0]
	v_pk_mul_f32 v[74:75], v[88:89], v[46:47] op_sel:[0,1] op_sel_hi:[0,0] neg_lo:[0,1]
	v_pk_fma_f32 v[46:47], v[88:89], v[46:47], v[74:75] op_sel_hi:[0,1,1]
	v_pk_add_f32 v[74:75], v[96:97], v[52:53]
	v_pk_add_f32 v[52:53], v[96:97], v[52:53] neg_lo:[0,1] neg_hi:[0,1]
	v_add_f32_e32 v30, v30, v34
	v_pk_mul_f32 v[84:85], v[88:89], v[52:53] op_sel:[0,1] op_sel_hi:[0,0] neg_lo:[0,1]
	v_sub_f32_e32 v34, v16, v18
	v_sub_f32_e32 v13, v51, v61
	v_pk_fma_f32 v[52:53], v[88:89], v[52:53], v[84:85] op_sel_hi:[0,1,1] neg_lo:[1,0,0] neg_hi:[1,0,0]
	v_sub_f32_e32 v51, v34, v82
	v_sub_f32_e32 v25, v29, v43
	v_sub_f32_e32 v43, v31, v35
	v_sub_f32_e32 v35, v49, v59
	v_sub_f32_e32 v10, v47, v53
	v_add_f32_e32 v49, v50, v60
	v_add_f32_e32 v50, v68, v76
	v_add_f32_e32 v53, v51, v30
	v_sub_f32_e32 v23, v27, v37
	v_sub_f32_e32 v27, v55, v57
	v_add_f32_e32 v38, v38, v40
	v_add_f32_e32 v40, v78, v80
	v_add_f32_e32 v55, v53, v50
	v_add_f32_e32 v16, v55, v40
	v_sub_f32_e32 v41, v39, v41
	v_add_f32_e32 v21, v20, v38
	global_store_dword v[14:15], v16, off offset:2048
	v_add_co_u32_e32 v16, vcc, s10, v14
	v_add_f32_e32 v47, v66, v70
	v_add_f32_e32 v24, v21, v49
	v_add_f32_e32 v32, v32, v44
	v_sub_f32_e32 v44, v22, v41
	v_addc_co_u32_e32 v17, vcc, 0, v15, vcc
	v_pk_mul_f32 v[72:73], v[88:89], v[62:63] op_sel:[0,1] op_sel_hi:[0,0] neg_lo:[0,1]
	v_add_f32_e32 v19, v24, v47
	v_add_f32_e32 v54, v54, v56
	v_add_f32_e32 v56, v44, v32
	v_add_co_u32_e32 v18, vcc, s11, v14
	v_add_f32_e32 v34, v34, v82
	v_pk_fma_f32 v[62:63], v[88:89], v[62:63], v[72:73] op_sel_hi:[0,1,1]
	v_pk_add_f32 v[72:73], v[94:95], v[86:87]
	global_store_dword v[14:15], v19, off
	v_add_f32_e32 v57, v56, v54
	v_addc_co_u32_e32 v19, vcc, 0, v15, vcc
	v_add_f32_e32 v48, v48, v58
	v_sub_f32_e32 v58, v34, v43
	global_store_dword v[18:19], v57, off offset:-4096
	v_add_f32_e32 v57, v72, v74
	v_add_f32_e32 v59, v58, v48
	v_sub_f32_e32 v20, v20, v38
	v_sub_f32_e32 v37, v33, v45
	v_sub_f32_e32 v45, v69, v77
	v_add_f32_e32 v60, v59, v57
	v_add_f32_e32 v26, v26, v36
	v_sub_f32_e32 v36, v20, v13
	v_sub_f32_e32 v30, v51, v30
	global_store_dword v[16:17], v60, off offset:2048
	v_add_f32_e32 v16, v36, v26
	v_add_f32_e32 v38, v62, v64
	v_sub_f32_e32 v51, v30, v45
	global_store_dword v[18:19], v16, off
	v_add_f32_e32 v16, v51, v38
	global_store_dword v[18:19], v16, off offset:2048
	v_add_co_u32_e32 v16, vcc, s78, v14
	v_add_f32_e32 v22, v22, v41
	s_nop 0
	v_addc_co_u32_e32 v17, vcc, 0, v15, vcc
	v_add_f32_e32 v28, v28, v42
	v_sub_f32_e32 v41, v22, v37
	v_add_co_u32_e32 v18, vcc, s43, v14
	v_add_f32_e32 v42, v41, v28
	s_nop 0
	v_addc_co_u32_e32 v19, vcc, 0, v15, vcc
	v_add_f32_e32 v34, v34, v43
	global_store_dword v[18:19], v42, off offset:-4096
	v_add_f32_e32 v42, v46, v52
	v_sub_f32_e32 v43, v34, v35
	v_sub_f32_e32 v39, v67, v71
	v_add_f32_e32 v46, v43, v42
	v_sub_f32_e32 v21, v21, v49
	v_sub_f32_e32 v33, v79, v81
	global_store_dword v[16:17], v46, off offset:2048
	v_sub_f32_e32 v16, v21, v39
	v_sub_f32_e32 v46, v53, v50
	global_store_dword v[18:19], v16, off
	v_sub_f32_e32 v16, v46, v33
	global_store_dword v[18:19], v16, off offset:2048
	v_add_co_u32_e32 v16, vcc, s13, v14
	v_sub_f32_e32 v32, v44, v32
	s_nop 0
	v_addc_co_u32_e32 v17, vcc, 0, v15, vcc
	v_add_co_u32_e32 v18, vcc, s12, v14
	v_sub_f32_e32 v44, v32, v27
	s_nop 0
	v_addc_co_u32_e32 v19, vcc, 0, v15, vcc
	v_sub_f32_e32 v31, v73, v75
	global_store_dword v[18:19], v44, off offset:-4096
	v_sub_f32_e32 v44, v58, v48
	v_sub_f32_e32 v48, v44, v31
	v_add_f32_e32 v20, v20, v13
	v_sub_f32_e32 v29, v63, v65
	global_store_dword v[16:17], v48, off offset:2048
	v_sub_f32_e32 v13, v20, v23
	v_add_f32_e32 v30, v30, v45
	v_add_co_u32_e32 v16, vcc, s16, v14
	global_store_dword v[18:19], v13, off
	v_sub_f32_e32 v13, v30, v29
	v_addc_co_u32_e32 v17, vcc, 0, v15, vcc
	global_store_dword v[18:19], v13, off offset:2048
	v_add_f32_e32 v22, v22, v37
	v_add_co_u32_e32 v18, vcc, s8, v14
	v_sub_f32_e32 v13, v22, v25
	s_nop 0
	v_addc_co_u32_e32 v19, vcc, 0, v15, vcc
	global_store_dword v[18:19], v13, off offset:-4096
	v_add_f32_e32 v13, v34, v35
	v_sub_f32_e32 v34, v13, v10
	global_store_dword v[16:17], v34, off offset:2048
	v_sub_f32_e32 v16, v24, v47
	global_store_dword v[18:19], v16, off
	v_sub_f32_e32 v16, v55, v40
	global_store_dword v[18:19], v16, off offset:2048
	v_add_co_u32_e32 v16, vcc, s9, v14
	v_sub_f32_e32 v24, v56, v54
	s_nop 0
	v_addc_co_u32_e32 v17, vcc, 0, v15, vcc
	v_add_co_u32_e32 v18, vcc, s7, v14
	v_add_f32_e32 v10, v13, v10
	s_nop 0
	v_addc_co_u32_e32 v19, vcc, 0, v15, vcc
	global_store_dword v[18:19], v24, off offset:-4096
	v_sub_f32_e32 v24, v59, v57
	global_store_dword v[16:17], v24, off offset:2048
	v_sub_f32_e32 v16, v36, v26
	global_store_dword v[18:19], v16, off
	v_sub_f32_e32 v16, v51, v38
	global_store_dword v[18:19], v16, off offset:2048
	v_add_co_u32_e32 v16, vcc, s5, v14
	v_sub_f32_e32 v24, v41, v28
	s_nop 0
	v_addc_co_u32_e32 v17, vcc, 0, v15, vcc
	v_add_co_u32_e32 v18, vcc, s6, v14
	s_nop 1
	v_addc_co_u32_e32 v19, vcc, 0, v15, vcc
	global_store_dword v[18:19], v24, off offset:-4096
	v_sub_f32_e32 v24, v43, v42
	global_store_dword v[16:17], v24, off offset:2048
	v_add_f32_e32 v16, v21, v39
	global_store_dword v[18:19], v16, off
	v_add_f32_e32 v16, v46, v33
	global_store_dword v[18:19], v16, off offset:2048
	v_add_co_u32_e32 v16, vcc, s4, v14
	v_add_f32_e32 v21, v32, v27
	s_nop 0
	v_addc_co_u32_e32 v17, vcc, 0, v15, vcc
	v_add_co_u32_e32 v18, vcc, s1, v14
	s_nop 1
	v_addc_co_u32_e32 v19, vcc, 0, v15, vcc
	global_store_dword v[18:19], v21, off offset:-4096
	v_add_f32_e32 v21, v44, v31
	global_store_dword v[16:17], v21, off offset:2048
	v_add_f32_e32 v16, v20, v23
	global_store_dword v[18:19], v16, off
	v_add_f32_e32 v16, v30, v29
	v_add_co_u32_e32 v14, vcc, s0, v14
	global_store_dword v[18:19], v16, off offset:2048
	v_add_f32_e32 v16, v22, v25
	v_addc_co_u32_e32 v15, vcc, 0, v15, vcc
	global_store_dword v[14:15], v16, off
	global_store_dword v[14:15], v10, off offset:2048
	v_mov_b32_e32 v10, v183
	v_mov_b32_e32 v14, v184
	v_mov_b32_e32 v18, v182
	s_movk_i32 s0, 0xfe00
	v_sub_u32_e32 v13, 0x4000, v18
	v_cmp_eq_u32_e32 vcc, 0, v18
	v_cmp_eq_u32_e64 s[0:1], s0, v18
	v_cmp_eq_u32_e64 s[4:5], s48, v18
	v_cndmask_b32_e64 v20, v13, 0, vcc
	v_sub_u32_e32 v13, 0x3e00, v18
	v_cndmask_b32_e64 v22, v13, 0, s[0:1]
	v_sub_u32_e32 v13, 0x3c00, v18
	v_ashrrev_i32_e32 v21, 31, v20
	v_ashrrev_i32_e32 v23, 31, v22
	v_cndmask_b32_e64 v24, v13, 0, s[4:5]
	v_lshl_add_u64 v[20:21], v[20:21], 1, s[2:3]
	v_lshl_add_u64 v[22:23], v[22:23], 1, s[2:3]
	v_ashrrev_i32_e32 v25, 31, v24
	v_sub_u32_e32 v13, 0x3a00, v18
	v_cmp_eq_u32_e64 s[6:7], s49, v18
	v_lshl_add_u64 v[24:25], v[24:25], 1, s[2:3]
	global_load_ushort v15, v[20:21], off
	s_nop 0
	global_load_ushort v22, v[22:23], off
	s_nop 0
	global_load_ushort v23, v[24:25], off
	v_cndmask_b32_e64 v20, v13, 0, s[6:7]
	v_ashrrev_i32_e32 v21, 31, v20
	v_ashrrev_i32_e32 v19, 31, v18
	v_lshl_add_u64 v[20:21], v[20:21], 1, s[2:3]
	v_lshl_add_u64 v[16:17], v[18:19], 1, s[76:77]
	global_load_ushort v20, v[20:21], off
	s_nop 0
	global_load_ushort v13, v[16:17], off offset:3072
	v_sub_u32_e32 v24, 0x3800, v18
	v_sub_u32_e32 v26, 0x3600, v18
	v_sub_u32_e32 v28, 0x3400, v18
	v_sub_u32_e32 v32, 0x3200, v18
	v_cmp_eq_u32_e64 s[8:9], s59, v18
	s_mov_b32 s48, s21
	s_mov_b32 s49, s20
	s_mov_b32 s59, s82
	s_waitcnt vmcnt(4)
	v_lshlrev_b32_e32 v15, 16, v15
	v_cndmask_b32_e64 v19, -v15, v15, vcc
	s_waitcnt vmcnt(3)
	v_lshlrev_b32_e32 v15, 16, v22
	v_cndmask_b32_e64 v31, -v15, v15, s[0:1]
	s_waitcnt vmcnt(2)
	v_lshlrev_b32_e32 v15, 16, v23
	v_cndmask_b32_e64 v30, -v15, v15, s[4:5]
	v_cmp_eq_u32_e64 s[4:5], s51, v18
	s_waitcnt vmcnt(1)
	v_lshlrev_b32_e32 v15, 16, v20
	v_add_co_u32_e32 v20, vcc, s10, v16
	v_cndmask_b32_e64 v15, -v15, v15, s[6:7]
	s_nop 0
	v_addc_co_u32_e32 v21, vcc, 0, v17, vcc
	v_add_co_u32_e32 v22, vcc, s11, v16
	v_cmp_eq_u32_e64 s[6:7], s50, v18
	s_nop 0
	v_addc_co_u32_e32 v23, vcc, 0, v17, vcc
	v_cmp_eq_u32_e64 s[0:1], s57, v18
	v_cndmask_b32_e64 v24, v24, 0, s[6:7]
	v_cndmask_b32_e64 v26, v26, 0, s[4:5]
	v_cndmask_b32_e64 v28, v28, 0, s[0:1]
	v_cmp_eq_u32_e32 vcc, s58, v18
	v_ashrrev_i32_e32 v25, 31, v24
	v_ashrrev_i32_e32 v27, 31, v26
	v_ashrrev_i32_e32 v29, 31, v28
	v_cndmask_b32_e64 v32, v32, 0, vcc
	v_lshl_add_u64 v[24:25], v[24:25], 1, s[2:3]
	v_lshl_add_u64 v[26:27], v[26:27], 1, s[2:3]
	v_lshl_add_u64 v[28:29], v[28:29], 1, s[2:3]
	v_ashrrev_i32_e32 v33, 31, v32
	v_lshl_add_u64 v[32:33], v[32:33], 1, s[2:3]
	global_load_ushort v34, v[24:25], off
	s_nop 0
	global_load_ushort v26, v[26:27], off
	s_nop 0
	global_load_ushort v27, v[28:29], off
	s_nop 0
	global_load_ushort v28, v[32:33], off
	v_sub_u32_e32 v24, 0x3000, v18
	v_cndmask_b32_e64 v24, v24, 0, s[8:9]
	v_ashrrev_i32_e32 v25, 31, v24
	v_lshl_add_u64 v[24:25], v[24:25], 1, s[2:3]
	global_load_ushort v24, v[24:25], off
	s_nop 0
	global_load_ushort v32, v[20:21], off offset:3072
	v_cmp_eq_u32_e64 s[10:11], s79, v18
	s_mov_b32 s79, s80
	s_waitcnt vmcnt(6)
	v_lshlrev_b32_e32 v13, 16, v13
	s_mov_b32 s57, s18
	s_mov_b32 s58, s83
	s_waitcnt vmcnt(5)
	v_lshlrev_b32_e32 v25, 16, v34
	v_cndmask_b32_e64 v33, -v25, v25, s[6:7]
	s_waitcnt vmcnt(4)
	v_lshlrev_b32_e32 v25, 16, v26
	v_cndmask_b32_e64 v34, -v25, v25, s[4:5]
	s_waitcnt vmcnt(3)
	v_lshlrev_b32_e32 v25, 16, v27
	v_cndmask_b32_e64 v35, -v25, v25, s[0:1]
	v_add_co_u32_e64 v26, s[0:1], s78, v16
	s_waitcnt vmcnt(2)
	v_lshlrev_b32_e32 v25, 16, v28
	s_waitcnt vmcnt(1)
	v_lshlrev_b32_e32 v24, 16, v24
	v_addc_co_u32_e64 v27, s[0:1], 0, v17, s[0:1]
	v_cndmask_b32_e64 v36, -v25, v25, vcc
	v_cndmask_b32_e64 v37, -v24, v24, s[8:9]
	v_sub_u32_e32 v24, 0x2e00, v18
	v_cmp_eq_u32_e32 vcc, s60, v18
	v_sub_u32_e32 v28, 0x2c00, v18
	v_cmp_eq_u32_e64 s[0:1], s61, v18
	v_cndmask_b32_e64 v24, v24, 0, vcc
	v_ashrrev_i32_e32 v25, 31, v24
	v_cndmask_b32_e64 v28, v28, 0, s[0:1]
	v_ashrrev_i32_e32 v29, 31, v28
	v_lshl_add_u64 v[24:25], v[24:25], 1, s[2:3]
	v_lshl_add_u64 v[28:29], v[28:29], 1, s[2:3]
	global_load_ushort v41, v[24:25], off
	s_nop 0
	global_load_ushort v28, v[28:29], off
	v_sub_u32_e32 v24, 0x2a00, v18
	v_cmp_eq_u32_e64 s[4:5], s62, v18
	v_cmp_eq_u32_e64 s[6:7], s63, v18
	v_cmp_eq_u32_e64 s[8:9], s68, v18
	v_cndmask_b32_e64 v24, v24, 0, s[4:5]
	v_ashrrev_i32_e32 v25, 31, v24
	v_lshl_add_u64 v[24:25], v[24:25], 1, s[2:3]
	global_load_ushort v29, v[24:25], off
	v_sub_u32_e32 v24, 0x2800, v18
	v_cndmask_b32_e64 v24, v24, 0, s[6:7]
	v_ashrrev_i32_e32 v25, 31, v24
	v_lshl_add_u64 v[24:25], v[24:25], 1, s[2:3]
	global_load_ushort v38, v[26:27], off offset:1024
	global_load_ushort v40, v[26:27], off offset:2048
	global_load_ushort v39, v[26:27], off offset:3072
	global_load_ushort v44, v[24:25], off
	v_sub_u32_e32 v26, 0x2600, v18
	s_mov_b32 s78, s81
	s_mov_b32 s60, s87
	s_mov_b32 s61, s86
	s_mov_b32 s68, s89
	s_mov_b32 s62, s93
	s_mov_b32 s63, s92
	s_waitcnt vmcnt(6)
	v_lshlrev_b32_e32 v24, 16, v41
	v_cndmask_b32_e64 v43, -v24, v24, vcc
	s_waitcnt vmcnt(5)
	v_lshlrev_b32_e32 v24, 16, v28
	v_cndmask_b32_e64 v41, -v24, v24, s[0:1]
	v_add_co_u32_e64 v28, s[0:1], s13, v16
	s_waitcnt vmcnt(4)
	v_lshlrev_b32_e32 v24, 16, v29
	v_cndmask_b32_e64 v42, -v24, v24, s[4:5]
	v_add_co_u32_e32 v24, vcc, s43, v16
	v_addc_co_u32_e64 v29, s[0:1], 0, v17, s[0:1]
	s_nop 0
	v_addc_co_u32_e32 v25, vcc, 0, v17, vcc
	v_cmp_eq_u32_e32 vcc, s66, v18
	v_cmp_eq_u32_e64 s[4:5], s74, v18
	v_cmp_eq_u32_e64 s[0:1], s75, v18
	v_cndmask_b32_e64 v26, v26, 0, vcc
	v_ashrrev_i32_e32 v27, 31, v26
	v_lshl_add_u64 v[26:27], v[26:27], 1, s[2:3]
	global_load_ushort v26, v[26:27], off
	s_waitcnt vmcnt(1)
	v_lshlrev_b32_e32 v27, 16, v44
	v_sub_u32_e32 v44, 0x2200, v18
	v_cndmask_b32_e64 v45, -v27, v27, s[6:7]
	v_cndmask_b32_e64 v46, v44, 0, s[8:9]
	v_sub_u32_e32 v44, 0x2000, v18
	v_cmp_eq_u32_e64 s[6:7], s69, v18
	v_ashrrev_i32_e32 v47, 31, v46
	v_lshl_add_u64 v[46:47], v[46:47], 1, s[2:3]
	v_cndmask_b32_e64 v50, v44, 0, s[6:7]
	v_sub_u32_e32 v44, 0x1e00, v18
	v_cndmask_b32_e64 v52, v44, 0, s[4:5]
	v_sub_u32_e32 v44, 0x1c00, v18
	v_ashrrev_i32_e32 v51, 31, v50
	v_cndmask_b32_e64 v54, v44, 0, s[0:1]
	v_lshl_add_u64 v[50:51], v[50:51], 1, s[2:3]
	v_ashrrev_i32_e32 v53, 31, v52
	v_ashrrev_i32_e32 v55, 31, v54
	v_lshl_add_u64 v[52:53], v[52:53], 1, s[2:3]
	v_lshl_add_u64 v[54:55], v[54:55], 1, s[2:3]
	s_mov_b32 s66, s25
	s_mov_b32 s69, s88
	s_mov_b32 s74, s29
	s_mov_b32 s75, s28
	s_movk_i32 s43, 0x6000
	s_waitcnt vmcnt(0)
	v_lshlrev_b32_e32 v26, 16, v26
	v_cndmask_b32_e64 v49, -v26, v26, vcc
	v_sub_u32_e32 v26, 0x2400, v18
	v_cmp_eq_u32_e32 vcc, s67, v18
	s_mov_b32 s67, s24
	s_nop 0
	v_cndmask_b32_e64 v26, v26, 0, vcc
	v_ashrrev_i32_e32 v27, 31, v26
	v_lshl_add_u64 v[26:27], v[26:27], 1, s[2:3]
	global_load_ushort v44, v[26:27], off
	s_nop 0
	global_load_ushort v46, v[46:47], off
	s_nop 0
	global_load_ushort v47, v[50:51], off
	global_load_ushort v48, v[52:53], off
	s_nop 0
	global_load_ushort v50, v[54:55], off
	v_sub_u32_e32 v26, 0x1a00, v18
	v_cndmask_b32_e64 v26, v26, 0, s[10:11]
	v_ashrrev_i32_e32 v27, 31, v26
	v_lshl_add_u64 v[26:27], v[26:27], 1, s[2:3]
	global_load_ushort v26, v[26:27], off
	s_nop 0
	global_load_ushort v53, v[28:29], off offset:1024
	global_load_ushort v51, v[28:29], off offset:2048
	s_waitcnt vmcnt(7)
	v_lshlrev_b32_e32 v27, 16, v44
	v_cndmask_b32_e64 v61, -v27, v27, vcc
	s_waitcnt vmcnt(6)
	v_lshlrev_b32_e32 v27, 16, v46
	v_cndmask_b32_e64 v63, -v27, v27, s[8:9]
	s_waitcnt vmcnt(5)
	v_lshlrev_b32_e32 v27, 16, v47
	v_cndmask_b32_e64 v90, -v27, v27, s[6:7]
	s_waitcnt vmcnt(4)
	v_lshlrev_b32_e32 v27, 16, v48
	v_cndmask_b32_e64 v59, -v27, v27, s[4:5]
	s_waitcnt vmcnt(3)
	v_lshlrev_b32_e32 v27, 16, v50
	v_cndmask_b32_e64 v57, -v27, v27, s[0:1]
	v_sub_u32_e32 v44, 0x1800, v18
	v_cmp_eq_u32_e64 s[8:9], s56, v18
	s_movk_i32 s0, 0xd600
	s_waitcnt vmcnt(2)
	v_lshlrev_b32_e32 v26, 16, v26
	v_cndmask_b32_e64 v46, v44, 0, s[8:9]
	v_sub_u32_e32 v44, 0x1600, v18
	v_cmp_eq_u32_e64 s[6:7], s0, v18
	s_movk_i32 s0, 0xd400
	v_cndmask_b32_e64 v55, -v26, v26, s[10:11]
	v_add_co_u32_e32 v26, vcc, s12, v16
	v_cndmask_b32_e64 v64, v44, 0, s[6:7]
	v_sub_u32_e32 v44, 0x1400, v18
	v_cmp_eq_u32_e64 s[4:5], s0, v18
	s_movk_i32 s0, 0xd200
	v_addc_co_u32_e32 v27, vcc, 0, v17, vcc
	v_cndmask_b32_e64 v66, v44, 0, s[4:5]
	v_sub_u32_e32 v44, 0x1200, v18
	v_cmp_eq_u32_e64 s[0:1], s0, v18
	s_movk_i32 s10, 0xd000
	v_cmp_eq_u32_e32 vcc, s10, v18
	v_cndmask_b32_e64 v68, v44, 0, s[0:1]
	v_sub_u32_e32 v44, 0x1000, v18
	v_ashrrev_i32_e32 v47, 31, v46
	v_cndmask_b32_e64 v70, v44, 0, vcc
	v_lshl_add_u64 v[46:47], v[46:47], 1, s[2:3]
	v_ashrrev_i32_e32 v65, 31, v64
	v_ashrrev_i32_e32 v67, 31, v66
	v_ashrrev_i32_e32 v69, 31, v68
	v_ashrrev_i32_e32 v71, 31, v70
	v_lshl_add_u64 v[64:65], v[64:65], 1, s[2:3]
	v_lshl_add_u64 v[66:67], v[66:67], 1, s[2:3]
	v_lshl_add_u64 v[68:69], v[68:69], 1, s[2:3]
	v_lshl_add_u64 v[70:71], v[70:71], 1, s[2:3]
	global_load_ushort v44, v[46:47], off
	global_load_ushort v48, v[64:65], off
	global_load_ushort v50, v[66:67], off
	global_load_ushort v52, v[68:69], off
	global_load_ushort v54, v[70:71], off
	v_sub_u32_e32 v46, 0xe00, v18
	v_cmp_eq_u32_e64 s[12:13], s84, v18
	s_movk_i32 s10, 0xcc00
	v_cmp_eq_u32_e64 s[10:11], s10, v18
	v_cndmask_b32_e64 v46, v46, 0, s[12:13]
	v_ashrrev_i32_e32 v47, 31, v46
	v_lshl_add_u64 v[46:47], v[46:47], 1, s[2:3]
	global_load_ushort v56, v[46:47], off
	v_sub_u32_e32 v46, 0xc00, v18
	v_cndmask_b32_e64 v46, v46, 0, s[10:11]
	v_ashrrev_i32_e32 v47, 31, v46
	v_lshl_add_u64 v[46:47], v[46:47], 1, s[2:3]
	global_load_ushort v46, v[46:47], off
	s_nop 0
	global_load_ushort v91, v[28:29], off offset:3072
	s_mov_b32 s84, 0x3f3504f3
	s_mov_b32 s85, 0xbf3504f3
	s_mov_b32 s54, s85
	s_mov_b32 s55, s84
	s_mov_b32 s56, s19
	s_mov_b32 s38, s85
	s_waitcnt vmcnt(7)
	v_lshlrev_b32_e32 v28, 16, v44
	v_cndmask_b32_e64 v97, -v28, v28, s[8:9]
	s_waitcnt vmcnt(6)
	v_lshlrev_b32_e32 v28, 16, v48
	v_cndmask_b32_e64 v96, -v28, v28, s[6:7]
	s_waitcnt vmcnt(5)
	v_lshlrev_b32_e32 v28, 16, v50
	v_cndmask_b32_e64 v94, -v28, v28, s[4:5]
	s_waitcnt vmcnt(4)
	v_lshlrev_b32_e32 v28, 16, v52
	v_cndmask_b32_e64 v93, -v28, v28, s[0:1]
	s_waitcnt vmcnt(3)
	v_lshlrev_b32_e32 v28, 16, v54
	v_cndmask_b32_e64 v92, -v28, v28, vcc
	s_movk_i32 s0, 0xca00
	v_cmp_eq_u32_e64 s[0:1], s0, v18
	s_waitcnt vmcnt(2)
	v_lshlrev_b32_e32 v28, 16, v56
	v_cndmask_b32_e64 v95, -v28, v28, s[12:13]
	v_sub_u32_e32 v28, 0xa00, v18
	v_cndmask_b32_e64 v28, v28, 0, s[0:1]
	v_ashrrev_i32_e32 v29, 31, v28
	v_lshl_add_u64 v[28:29], v[28:29], 1, s[2:3]
	global_load_ushort v44, v[28:29], off
	s_waitcnt vmcnt(2)
	v_lshlrev_b32_e32 v28, 16, v46
	v_cndmask_b32_e64 v106, -v28, v28, s[10:11]
	v_add_co_u32_e32 v28, vcc, s16, v16
	s_movk_i32 s4, 0xc400
	s_nop 0
	v_addc_co_u32_e32 v29, vcc, 0, v17, vcc
	v_sub_u32_e32 v46, 0x400, v18
	v_cmp_eq_u32_e32 vcc, s4, v18
	s_movk_i32 s4, 0xc800
	v_sub_u32_e32 v48, 0x800, v18
	v_cndmask_b32_e64 v46, v46, 0, vcc
	v_cmp_eq_u32_e64 s[4:5], s4, v18
	v_ashrrev_i32_e32 v47, 31, v46
	v_lshl_add_u64 v[46:47], v[46:47], 1, s[2:3]
	v_cndmask_b32_e64 v64, v48, 0, s[4:5]
	v_ashrrev_i32_e32 v65, 31, v64
	v_lshl_add_u64 v[64:65], v[64:65], 1, s[2:3]
	global_load_ushort v48, v[46:47], off
	s_nop 0
	global_load_ushort v46, v[64:65], off
	global_load_ushort v110, v[28:29], off
	global_load_ushort v112, v[28:29], off offset:1024
	global_load_ushort v114, v[28:29], off offset:2048
	global_load_ushort v116, v[28:29], off offset:3072
	s_mov_b32 s6, 0x3f7b14be
	s_mov_b32 s7, 0xbe47c5c2
	s_mov_b32 s16, 0x3f6c835e
	s_mov_b32 s17, 0xbec3ef15
	s_mov_b32 s50, s17
	s_mov_b32 s51, s16
	v_add_f32_e32 v50, v15, v13
	s_mov_b32 s8, 0x3e47c5c2
	s_mov_b32 s9, 0xbf7b14be
	s_mov_b32 s30, s9
	s_mov_b32 s31, s8
	s_mov_b32 s10, s93
	s_mov_b32 s11, s81
	s_mov_b32 s12, s17
	s_mov_b32 s13, s19
	s_waitcnt vmcnt(6)
	v_lshlrev_b32_e32 v28, 16, v44
	v_cndmask_b32_e64 v108, -v28, v28, s[0:1]
	s_movk_i32 s0, 0xc600
	v_sub_u32_e32 v28, 0x600, v18
	v_sub_u32_e32 v44, 0x200, v18
	s_waitcnt vmcnt(4)
	v_lshlrev_b32_e32 v29, 16, v46
	v_cndmask_b32_e64 v111, -v29, v29, s[4:5]
	v_cmp_eq_u32_e64 s[4:5], s0, v18
	s_movk_i32 s0, 0xc200
	v_cmp_eq_u32_e64 s[0:1], s0, v18
	v_cndmask_b32_e64 v28, v28, 0, s[4:5]
	v_ashrrev_i32_e32 v29, 31, v28
	v_cndmask_b32_e64 v46, v44, 0, s[0:1]
	v_lshl_add_u64 v[28:29], v[28:29], 1, s[2:3]
	v_ashrrev_i32_e32 v47, 31, v46
	v_lshl_add_u64 v[46:47], v[46:47], 1, s[2:3]
	global_load_ushort v18, v[16:17], off
	s_nop 0
	global_load_ushort v28, v[28:29], off
	s_nop 0
	global_load_ushort v29, v[16:17], off offset:1024
	s_nop 0
	global_load_ushort v17, v[16:17], off offset:2048
	s_nop 0
	global_load_ushort v44, v[46:47], off
	global_load_ushort v58, v[22:23], off offset:1024
	global_load_ushort v62, v[22:23], off offset:2048
	global_load_ushort v68, v[22:23], off offset:3072
	global_load_ushort v69, v[24:25], off offset:-4096
	global_load_ushort v98, v[24:25], off
	global_load_ushort v52, v[22:23], off offset:-4096
	global_load_ushort v54, v[20:21], off offset:1024
	s_nop 0
	global_load_ushort v21, v[20:21], off offset:2048
	s_nop 0
	global_load_ushort v56, v[22:23], off
	s_mov_b32 s2, 0x3f7ec46d
	s_mov_b32 s3, 0xbdc8bd36
	v_lshlrev_b32_e32 v22, 16, v48
	s_mov_b32 s76, s3
	s_mov_b32 s77, s2
	v_cndmask_b32_e64 v115, -v22, v22, vcc
	v_pk_mul_f32 v[22:23], v[14:15], s[76:77] op_sel_hi:[0,1] neg_lo:[1,0]
	s_mov_b64 vcc, s[64:65]
	s_mov_b32 s64, s7
	s_mov_b32 s65, s6
	s_waitcnt vmcnt(13)
	v_lshlrev_b32_e32 v16, 16, v18
	s_waitcnt vmcnt(12)
	v_lshlrev_b32_e32 v18, 16, v28
	s_waitcnt vmcnt(11)
	v_lshlrev_b32_e32 v20, 16, v29
	s_waitcnt vmcnt(10)
	v_lshlrev_b32_e32 v17, 16, v17
	v_add_f32_e32 v20, v31, v20
	v_pk_fma_f32 v[28:29], v[10:11], s[2:3], v[22:23] op_sel_hi:[0,1,1]
	v_add_f32_e32 v22, v30, v17
	v_pk_mul_f32 v[30:31], v[14:15], s[64:65] op_sel_hi:[0,1] neg_lo:[1,0]
	v_pk_fma_f32 v[46:47], v[10:11], s[6:7], v[30:31] op_sel_hi:[0,1,1]
	v_pk_mul_f32 v[30:31], v[14:15], s[78:79] op_sel_hi:[0,1] neg_lo:[1,0]
	v_pk_fma_f32 v[88:89], v[10:11], s[80:81], v[30:31] op_sel_hi:[0,1,1]
	s_waitcnt vmcnt(3)
	v_lshlrev_b32_e32 v13, 16, v52
	v_pk_mul_f32 v[30:31], v[14:15], s[50:51] op_sel_hi:[0,1] neg_lo:[1,0]
	v_add_f32_e32 v16, v19, v16
	v_cndmask_b32_e64 v113, -v18, v18, s[4:5]
	v_pk_mul_f32 v[18:19], v[14:15], s[40:41] op_sel_hi:[0,1] neg_lo:[1,0]
	v_add_f32_e32 v52, v33, v13
	v_pk_fma_f32 v[84:85], v[10:11], s[16:17], v[30:31] op_sel_hi:[0,1,1]
	s_waitcnt vmcnt(2)
	v_lshlrev_b32_e32 v13, 16, v54
	v_pk_mul_f32 v[30:31], v[14:15], s[48:49] op_sel_hi:[0,1] neg_lo:[1,0]
	s_waitcnt vmcnt(1)
	v_lshlrev_b32_e32 v15, 16, v21
	v_lshlrev_b32_e32 v17, 16, v44
	v_add_f32_e32 v44, v34, v13
	global_load_ushort v13, v[24:25], off offset:1024
	global_load_ushort v33, v[26:27], off
	v_add_f32_e32 v48, v35, v15
	global_load_ushort v15, v[24:25], off offset:2048
	v_lshlrev_b32_e32 v21, 16, v32
	s_waitcnt vmcnt(3)
	v_lshlrev_b32_e32 v23, 16, v56
	v_add_f32_e32 v54, v36, v21
	global_load_ushort v21, v[24:25], off offset:3072
	v_add_f32_e32 v56, v37, v23
	v_lshlrev_b32_e32 v23, 16, v58
	v_add_f32_e32 v60, v43, v23
	global_load_ushort v23, v[26:27], off offset:-4096
	v_pk_fma_f32 v[64:65], v[10:11], s[20:21], v[30:31] op_sel_hi:[0,1,1]
	s_mov_b32 s4, 0x3dc8bd36
	s_mov_b32 s5, 0xbf7ec46d
	s_mov_b32 s34, s5
	s_mov_b32 s35, s4
	s_mov_b32 s2, s5
	v_cndmask_b32_e64 v17, -v17, v17, s[0:1]
	s_mov_b32 s0, s3
	s_mov_b32 s1, s5
	s_mov_b32 s6, s9
	s_mov_b32 s16, s19
	s_mov_b32 s20, s89
	v_pk_fma_f32 v[18:19], v[10:11], s[44:45], v[18:19] op_sel_hi:[0,1,1]
	s_waitcnt vmcnt(4)
	v_lshlrev_b32_e32 v13, 16, v13
	s_waitcnt vmcnt(2)
	v_pk_mul_f32 v[24:25], v[14:15], s[54:55] op_sel_hi:[0,1] neg_lo:[1,0]
	v_pk_fma_f32 v[78:79], v[10:11], s[84:85], v[24:25] op_sel_hi:[0,1,1]
	v_pk_mul_f32 v[24:25], v[14:15], s[60:61] op_sel_hi:[0,1] neg_lo:[1,0]
	v_pk_fma_f32 v[86:87], v[10:11], s[86:87], v[24:25] op_sel_hi:[0,1,1]
	v_lshlrev_b32_e32 v24, 16, v62
	v_add_f32_e32 v62, v41, v24
	v_pk_mul_f32 v[24:25], v[14:15], s[66:67] op_sel_hi:[0,1] neg_lo:[1,0]
	v_pk_fma_f32 v[82:83], v[10:11], s[24:25], v[24:25] op_sel_hi:[0,1,1]
	v_lshlrev_b32_e32 v24, 16, v68
	v_add_f32_e32 v58, v42, v24
	v_pk_mul_f32 v[24:25], v[14:15], s[68:69] op_sel_hi:[0,1] neg_lo:[1,0]
	v_pk_fma_f32 v[80:81], v[10:11], s[88:89], v[24:25] op_sel_hi:[0,1,1]
	v_lshlrev_b32_e32 v24, 16, v69
	v_add_f32_e32 v42, v45, v24
	v_pk_mul_f32 v[24:25], v[14:15], s[56:57] op_sel_hi:[0,1] neg_lo:[1,0]
	v_pk_fma_f32 v[74:75], v[10:11], s[18:19], v[24:25] op_sel_hi:[0,1,1]
	v_lshlrev_b32_e32 v24, 16, v38
	v_add_f32_e32 v38, v49, v24
	v_pk_mul_f32 v[24:25], v[14:15], s[62:63] op_sel_hi:[0,1] neg_lo:[1,0]
	v_pk_fma_f32 v[72:73], v[10:11], s[92:93], v[24:25] op_sel_hi:[0,1,1]
	v_lshlrev_b32_e32 v25, 16, v39
	v_add_f32_e32 v32, v63, v25
	global_load_ushort v25, v[26:27], off offset:1024
	global_load_ushort v39, v[26:27], off offset:2048
	v_lshlrev_b32_e32 v24, 16, v40
	global_load_ushort v40, v[26:27], off offset:3072
	v_pk_mul_f32 v[30:31], v[14:15], s[58:59] op_sel_hi:[0,1] neg_lo:[1,0]
	v_pk_fma_f32 v[66:67], v[10:11], s[82:83], v[30:31] op_sel_hi:[0,1,1]
	v_pk_mul_f32 v[30:31], v[14:15], s[74:75] op_sel_hi:[0,1] neg_lo:[1,0]
	v_pk_fma_f32 v[76:77], v[10:11], s[28:29], v[30:31] op_sel_hi:[0,1,1]
	v_pk_mul_f32 v[30:31], v[14:15], s[30:31] op_sel_hi:[0,1] neg_lo:[1,0]
	v_pk_fma_f32 v[68:69], v[10:11], s[8:9], v[30:31] op_sel_hi:[0,1,1]
	v_pk_mul_f32 v[30:31], v[14:15], s[34:35] op_sel_hi:[0,1] neg_lo:[1,0]
	v_pk_fma_f32 v[70:71], v[10:11], s[4:5], v[30:31] op_sel_hi:[0,1,1]
	v_lshlrev_b32_e32 v30, 16, v98
	v_pk_mul_f32 v[34:35], v[14:15], s[36:37] op_sel_hi:[0,1] neg_lo:[1,0]
	v_add_f32_e32 v30, v90, v30
	v_pk_fma_f32 v[34:35], v[10:11], s[96:97], v[34:35] op_sel_hi:[0,1,1]
	v_pk_mul_f32 v[36:37], v[34:35], v[30:31] op_sel_hi:[1,0]
	v_pk_mul_f32 v[30:31], v[14:15], s[2:3] op_sel_hi:[0,1] neg_lo:[1,0]
	v_add_f32_e32 v26, v59, v13
	v_pk_fma_f32 v[30:31], v[10:11], s[0:1], v[30:31] op_sel_hi:[0,1,1]
	v_lshlrev_b32_e32 v13, 16, v15
	s_mov_b32 s4, s7
	s_mov_b32 s5, s9
	v_pk_mul_f32 v[34:35], v[14:15], s[6:7] op_sel_hi:[0,1] neg_lo:[1,0]
	v_pk_mul_f32 v[26:27], v[30:31], v[26:27] op_sel_hi:[1,0]
	v_add_f32_e32 v30, v57, v13
	v_pk_fma_f32 v[34:35], v[10:11], s[4:5], v[34:35] op_sel_hi:[0,1,1]
	v_pk_mul_f32 v[98:99], v[34:35], v[30:31] op_sel_hi:[1,0]
	s_waitcnt vmcnt(4)
	v_lshlrev_b32_e32 v13, 16, v21
	s_mov_b32 s8, s81
	s_mov_b32 s9, s93
	v_pk_mul_f32 v[34:35], v[14:15], s[10:11] op_sel_hi:[0,1] neg_lo:[1,0]
	v_add_f32_e32 v30, v55, v13
	v_pk_fma_f32 v[34:35], v[10:11], s[8:9], v[34:35] op_sel_hi:[0,1,1]
	v_pk_mul_f32 v[100:101], v[34:35], v[30:31] op_sel_hi:[1,0]
	s_waitcnt vmcnt(3)
	v_lshlrev_b32_e32 v13, 16, v23
	v_pk_mul_f32 v[34:35], v[14:15], s[16:17] op_sel_hi:[0,1] neg_lo:[1,0]
	v_add_f32_e32 v30, v97, v13
	v_pk_fma_f32 v[34:35], v[10:11], s[12:13], v[34:35] op_sel_hi:[0,1,1]
	v_pk_mul_f32 v[102:103], v[34:35], v[30:31] op_sel_hi:[1,0]
	v_lshlrev_b32_e32 v13, 16, v53
	s_mov_b32 s18, s21
	s_mov_b32 s19, s89
	v_pk_mul_f32 v[34:35], v[14:15], s[20:21] op_sel_hi:[0,1] neg_lo:[1,0]
	v_add_f32_e32 v30, v96, v13
	v_pk_fma_f32 v[34:35], v[10:11], s[18:19], v[34:35] op_sel_hi:[0,1,1]
	s_mov_b32 s24, s25
	s_mov_b32 s25, s83
	v_pk_mul_f32 v[96:97], v[34:35], v[30:31] op_sel_hi:[1,0]
	v_lshlrev_b32_e32 v13, 16, v51
	v_pk_mul_f32 v[34:35], v[14:15], s[24:25] op_sel_hi:[0,1] neg_lo:[1,0]
	v_add_f32_e32 v30, v94, v13
	v_pk_fma_f32 v[34:35], v[10:11], s[22:23], v[34:35] op_sel_hi:[0,1,1]
	s_mov_b32 s28, s87
	v_pk_mul_f32 v[104:105], v[34:35], v[30:31] op_sel_hi:[1,0]
	v_lshlrev_b32_e32 v13, 16, v91
	v_pk_mul_f32 v[34:35], v[14:15], s[28:29] op_sel_hi:[0,1] neg_lo:[1,0]
	v_add_f32_e32 v30, v93, v13
	v_pk_fma_f32 v[34:35], v[10:11], s[26:27], v[34:35] op_sel_hi:[0,1,1]
	v_pk_mul_f32 v[90:91], v[34:35], v[30:31] op_sel_hi:[1,0]
	v_lshlrev_b32_e32 v13, 16, v33
	v_pk_mul_f32 v[34:35], v[14:15], s[84:85] op_sel_hi:[0,0] neg_lo:[1,0]
	v_add_f32_e32 v30, v92, v13
	v_pk_fma_f32 v[34:35], v[10:11], s[38:39], v[34:35] op_sel_hi:[0,0,1] neg_lo:[0,0,1] neg_hi:[0,0,1]
	v_pk_mul_f32 v[92:93], v[34:35], v[30:31] op_sel_hi:[1,0]
	v_pk_mul_f32 v[34:35], v[14:15], s[26:27] op_sel_hi:[0,1] neg_lo:[1,0]
	v_pk_fma_f32 v[34:35], v[10:11], s[28:29], v[34:35] op_sel_hi:[0,1,1]
	v_add_f32_e32 v24, v61, v24
	s_waitcnt vmcnt(2)
	v_lshlrev_b32_e32 v13, 16, v25
	v_add_f32_e32 v30, v95, v13
	v_pk_mul_f32 v[94:95], v[34:35], v[30:31] op_sel_hi:[1,0]
	s_waitcnt vmcnt(1)
	v_lshlrev_b32_e32 v13, 16, v39
	v_pk_mul_f32 v[34:35], v[14:15], s[22:23] op_sel_hi:[0,1] neg_lo:[1,0]
	v_add_f32_e32 v30, v106, v13
	v_pk_fma_f32 v[34:35], v[10:11], s[24:25], v[34:35] op_sel_hi:[0,1,1]
	v_pk_mul_f32 v[106:107], v[34:35], v[30:31] op_sel_hi:[1,0]
	s_waitcnt vmcnt(0)
	v_lshlrev_b32_e32 v13, 16, v40
	v_pk_mul_f32 v[34:35], v[14:15], s[18:19] op_sel_hi:[0,1] neg_lo:[1,0]
	v_add_f32_e32 v30, v108, v13
	v_pk_fma_f32 v[34:35], v[10:11], s[20:21], v[34:35] op_sel_hi:[0,1,1]
	v_pk_mul_f32 v[108:109], v[34:35], v[30:31] op_sel_hi:[1,0]
	v_lshlrev_b32_e32 v13, 16, v110
	v_pk_mul_f32 v[34:35], v[14:15], s[12:13] op_sel_hi:[0,1] neg_lo:[1,0]
	v_add_f32_e32 v30, v111, v13
	v_pk_fma_f32 v[34:35], v[10:11], s[16:17], v[34:35] op_sel_hi:[0,1,1]
	v_pk_mul_f32 v[110:111], v[34:35], v[30:31] op_sel_hi:[1,0]
	v_lshlrev_b32_e32 v13, 16, v112
	v_pk_mul_f32 v[34:35], v[14:15], s[8:9] op_sel_hi:[0,1] neg_lo:[1,0]
	v_add_f32_e32 v30, v113, v13
	v_pk_fma_f32 v[34:35], v[10:11], s[10:11], v[34:35] op_sel_hi:[0,1,1]
	v_pk_mul_f32 v[112:113], v[34:35], v[30:31] op_sel_hi:[1,0]
	v_lshlrev_b32_e32 v13, 16, v114
	v_pk_mul_f32 v[34:35], v[14:15], s[4:5] op_sel_hi:[0,1] neg_lo:[1,0]
	v_add_f32_e32 v30, v115, v13
	v_pk_fma_f32 v[34:35], v[10:11], s[6:7], v[34:35] op_sel_hi:[0,1,1]
	v_lshlrev_b32_e32 v13, 16, v116
	v_pk_mul_f32 v[14:15], v[14:15], s[0:1] op_sel_hi:[0,1] neg_lo:[1,0]
	v_pk_mul_f32 v[114:115], v[34:35], v[30:31] op_sel_hi:[1,0]
	v_add_f32_e32 v30, v17, v13
	v_pk_fma_f32 v[14:15], v[10:11], s[2:3], v[14:15] op_sel_hi:[0,1,1]
	v_pk_mul_f32 v[116:117], v[14:15], v[30:31] op_sel_hi:[1,0]
	v_mov_b32_e32 v13, v173
	v_mov_b32_e32 v30, v165
	v_mov_b32_e32 v10, v167
	v_mov_b32_e32 v34, v169
	v_mov_b32_e32 v17, v171
	s_nop 0
	v_pk_fma_f32 v[126:127], v[18:19], v[16:17], v[36:37] op_sel_hi:[1,0,1]
	v_pk_fma_f32 v[36:37], v[18:19], v[16:17], v[36:37] op_sel_hi:[1,0,1] neg_lo:[0,0,1] neg_hi:[0,0,1]
	v_pk_fma_f32 v[18:19], v[28:29], v[20:21], v[26:27] op_sel_hi:[1,0,1] neg_lo:[0,0,1] neg_hi:[0,0,1]
	v_pk_fma_f32 v[16:17], v[28:29], v[20:21], v[26:27] op_sel_hi:[1,0,1]
	v_pk_mul_f32 v[20:21], v[18:19], v[124:125] op_sel:[1,0] op_sel_hi:[0,0] neg_lo:[1,1] neg_hi:[0,1]
	s_nop 0
	v_pk_fma_f32 v[40:41], v[18:19], v[118:119], v[20:21] op_sel_hi:[1,0,1]
	v_pk_fma_f32 v[20:21], v[46:47], v[22:23], v[98:99] op_sel_hi:[1,0,1] neg_lo:[0,0,1] neg_hi:[0,0,1]
	v_pk_fma_f32 v[18:19], v[46:47], v[22:23], v[98:99] op_sel_hi:[1,0,1]
	v_pk_mul_f32 v[22:23], v[20:21], v[34:35] op_sel:[1,0] op_sel_hi:[0,0] neg_lo:[1,1] neg_hi:[0,1]
	s_nop 0
	v_pk_fma_f32 v[46:47], v[20:21], v[30:31], v[22:23] op_sel_hi:[1,0,1]
	v_pk_fma_f32 v[22:23], v[88:89], v[50:51], v[100:101] op_sel_hi:[1,0,1] neg_lo:[0,0,1] neg_hi:[0,0,1]
	v_pk_fma_f32 v[20:21], v[88:89], v[50:51], v[100:101] op_sel_hi:[1,0,1]
	v_pk_mul_f32 v[26:27], v[22:23], v[122:123] op_sel:[1,0] op_sel_hi:[0,0] neg_lo:[1,1] neg_hi:[0,1]
	s_nop 0
	v_pk_fma_f32 v[50:51], v[22:23], v[120:121], v[26:27] op_sel_hi:[1,0,1]
	v_pk_fma_f32 v[26:27], v[84:85], v[52:53], v[102:103] op_sel_hi:[1,0,1] neg_lo:[0,0,1] neg_hi:[0,0,1]
	v_pk_fma_f32 v[22:23], v[84:85], v[52:53], v[102:103] op_sel_hi:[1,0,1]
	v_pk_mul_f32 v[28:29], v[26:27], v[10:11] op_sel:[1,0] op_sel_hi:[0,0] neg_lo:[1,1] neg_hi:[0,1]
	s_nop 0
	v_pk_fma_f32 v[52:53], v[26:27], v[10:11], v[28:29] op_sel_hi:[1,0,1]
	v_pk_fma_f32 v[28:29], v[64:65], v[44:45], v[96:97] op_sel_hi:[1,0,1] neg_lo:[0,0,1] neg_hi:[0,0,1]
	v_pk_fma_f32 v[26:27], v[64:65], v[44:45], v[96:97] op_sel_hi:[1,0,1]
	v_pk_mul_f32 v[44:45], v[28:29], v[122:123] op_sel_hi:[1,0]
	s_nop 0
	v_pk_fma_f32 v[64:65], v[28:29], v[120:121], v[44:45] op_sel:[1,0,0] op_sel_hi:[0,0,1] neg_lo:[1,1,0] neg_hi:[0,1,0]
	v_pk_fma_f32 v[44:45], v[66:67], v[48:49], v[104:105] op_sel_hi:[1,0,1] neg_lo:[0,0,1] neg_hi:[0,0,1]
	v_pk_fma_f32 v[28:29], v[66:67], v[48:49], v[104:105] op_sel_hi:[1,0,1]
	v_pk_mul_f32 v[48:49], v[44:45], v[34:35] op_sel_hi:[1,0]
	s_nop 0
	v_pk_fma_f32 v[66:67], v[44:45], v[30:31], v[48:49] op_sel:[1,0,0] op_sel_hi:[0,0,1] neg_lo:[1,1,0] neg_hi:[0,1,0]
	v_pk_fma_f32 v[48:49], v[76:77], v[54:55], v[90:91] op_sel_hi:[1,0,1] neg_lo:[0,0,1] neg_hi:[0,0,1]
	v_pk_fma_f32 v[44:45], v[76:77], v[54:55], v[90:91] op_sel_hi:[1,0,1]
	v_pk_mul_f32 v[54:55], v[48:49], v[124:125] op_sel_hi:[1,0]
	v_xor_b32_e32 v76, 0x80000000, v49
	v_mov_b32_e32 v77, v48
	v_pk_fma_f32 v[48:49], v[78:79], v[56:57], v[92:93] op_sel_hi:[1,0,1]
	v_pk_fma_f32 v[56:57], v[78:79], v[56:57], v[92:93] op_sel_hi:[1,0,1] neg_lo:[0,0,1] neg_hi:[0,0,1]
	v_pk_fma_f32 v[54:55], v[76:77], v[118:119], v[54:55] op_sel_hi:[1,0,1] neg_lo:[0,1,0] neg_hi:[0,1,0]
	v_xor_b32_e32 v77, 0x80000000, v56
	v_mov_b32_e32 v76, v57
	v_pk_fma_f32 v[56:57], v[86:87], v[60:61], v[94:95] op_sel_hi:[1,0,1]
	v_pk_fma_f32 v[60:61], v[86:87], v[60:61], v[94:95] op_sel_hi:[1,0,1] neg_lo:[0,0,1] neg_hi:[0,0,1]
	s_nop 0
	v_pk_mul_f32 v[78:79], v[60:61], v[124:125] op_sel_hi:[1,0] neg_lo:[0,1] neg_hi:[0,1]
	s_nop 0
	v_pk_fma_f32 v[60:61], v[60:61], v[118:119], v[78:79] op_sel:[1,0,0] op_sel_hi:[0,0,1] neg_lo:[1,1,0] neg_hi:[0,1,0]
	v_pk_fma_f32 v[78:79], v[82:83], v[62:63], v[106:107] op_sel_hi:[1,0,1]
	v_pk_fma_f32 v[62:63], v[82:83], v[62:63], v[106:107] op_sel_hi:[1,0,1] neg_lo:[0,0,1] neg_hi:[0,0,1]
	s_nop 0
	v_pk_mul_f32 v[82:83], v[62:63], v[34:35] op_sel_hi:[1,0] neg_lo:[0,1] neg_hi:[0,1]
	s_nop 0
	v_pk_fma_f32 v[62:63], v[62:63], v[30:31], v[82:83] op_sel:[1,0,0] op_sel_hi:[0,0,1] neg_lo:[1,1,0] neg_hi:[0,1,0]
	v_pk_fma_f32 v[82:83], v[80:81], v[58:59], v[108:109] op_sel_hi:[1,0,1]
	v_pk_fma_f32 v[58:59], v[80:81], v[58:59], v[108:109] op_sel_hi:[1,0,1] neg_lo:[0,0,1] neg_hi:[0,0,1]
	s_nop 0
	v_pk_mul_f32 v[80:81], v[58:59], v[122:123] op_sel_hi:[1,0] neg_lo:[0,1] neg_hi:[0,1]
	s_nop 0
	v_pk_fma_f32 v[58:59], v[58:59], v[120:121], v[80:81] op_sel:[1,0,0] op_sel_hi:[0,0,1] neg_lo:[1,1,0] neg_hi:[0,1,0]
	v_pk_add_f32 v[84:85], v[16:17], v[56:57]
	v_pk_add_f32 v[16:17], v[16:17], v[56:57] neg_lo:[0,1] neg_hi:[0,1]
	v_pk_fma_f32 v[80:81], v[74:75], v[42:43], v[110:111] op_sel_hi:[1,0,1]
	v_pk_mul_f32 v[56:57], v[16:17], v[34:35] op_sel:[1,0] op_sel_hi:[0,0] neg_lo:[1,1] neg_hi:[0,1]
	v_pk_fma_f32 v[42:43], v[74:75], v[42:43], v[110:111] op_sel_hi:[1,0,1] neg_lo:[0,0,1] neg_hi:[0,0,1]
	v_pk_fma_f32 v[56:57], v[16:17], v[30:31], v[56:57] op_sel_hi:[1,0,1]
	v_pk_add_f32 v[16:17], v[18:19], v[78:79]
	v_pk_add_f32 v[18:19], v[18:19], v[78:79] neg_lo:[0,1] neg_hi:[0,1]
	v_pk_mul_f32 v[74:75], v[42:43], v[10:11] op_sel:[1,0] op_sel_hi:[0,0] neg_lo:[1,1] neg_hi:[0,1]
	v_pk_mul_f32 v[78:79], v[18:19], v[10:11] op_sel:[1,0] op_sel_hi:[0,0] neg_lo:[1,1] neg_hi:[0,1]
	v_pk_fma_f32 v[74:75], v[42:43], v[10:11], v[74:75] op_sel_hi:[1,0,1] neg_lo:[0,1,0] neg_hi:[0,1,0]
	v_pk_fma_f32 v[42:43], v[72:73], v[38:39], v[112:113] op_sel_hi:[1,0,1]
	v_pk_fma_f32 v[38:39], v[72:73], v[38:39], v[112:113] op_sel_hi:[1,0,1] neg_lo:[0,0,1] neg_hi:[0,0,1]
	v_pk_fma_f32 v[18:19], v[18:19], v[10:11], v[78:79] op_sel_hi:[1,0,1]
	v_pk_add_f32 v[78:79], v[20:21], v[82:83]
	v_pk_add_f32 v[20:21], v[20:21], v[82:83] neg_lo:[0,1] neg_hi:[0,1]
	s_nop 0
	v_pk_mul_f32 v[82:83], v[20:21], v[34:35] op_sel_hi:[1,0]
	v_xor_b32_e32 v86, 0x80000000, v21
	v_mov_b32_e32 v87, v20
	v_pk_add_f32 v[20:21], v[22:23], v[80:81]
	v_pk_add_f32 v[22:23], v[22:23], v[80:81] neg_lo:[0,1] neg_hi:[0,1]
	v_pk_mul_f32 v[72:73], v[38:39], v[122:123] op_sel:[1,0] op_sel_hi:[0,0] neg_lo:[1,1] neg_hi:[0,1]
	v_xor_b32_e32 v81, 0x80000000, v22
	v_mov_b32_e32 v80, v23
	v_pk_add_f32 v[22:23], v[26:27], v[42:43]
	v_pk_add_f32 v[26:27], v[26:27], v[42:43] neg_lo:[0,1] neg_hi:[0,1]
	v_pk_fma_f32 v[72:73], v[38:39], v[120:121], v[72:73] op_sel_hi:[1,0,1] neg_lo:[0,1,0] neg_hi:[0,1,0]
	v_pk_fma_f32 v[38:39], v[68:69], v[24:25], v[114:115] op_sel_hi:[1,0,1]
	v_pk_fma_f32 v[24:25], v[68:69], v[24:25], v[114:115] op_sel_hi:[1,0,1] neg_lo:[0,0,1] neg_hi:[0,0,1]
	v_pk_fma_f32 v[82:83], v[86:87], v[30:31], v[82:83] op_sel_hi:[1,0,1] neg_lo:[0,1,0] neg_hi:[0,1,0]
	v_pk_mul_f32 v[42:43], v[26:27], v[34:35] op_sel_hi:[1,0] neg_lo:[0,1] neg_hi:[0,1]
	s_nop 0
	v_pk_fma_f32 v[26:27], v[30:31], v[26:27], v[42:43] op_sel:[0,1,0] op_sel_hi:[0,0,1] neg_lo:[1,1,0] neg_hi:[1,0,0]
	v_pk_add_f32 v[42:43], v[28:29], v[38:39]
	v_pk_add_f32 v[28:29], v[28:29], v[38:39] neg_lo:[0,1] neg_hi:[0,1]
	v_pk_mul_f32 v[68:69], v[24:25], v[34:35] op_sel:[1,0] op_sel_hi:[0,0] neg_lo:[1,1] neg_hi:[0,1]
	v_pk_fma_f32 v[68:69], v[24:25], v[30:31], v[68:69] op_sel_hi:[1,0,1] neg_lo:[0,1,0] neg_hi:[0,1,0]
	v_pk_fma_f32 v[24:25], v[70:71], v[32:33], v[116:117] op_sel_hi:[1,0,1]
	v_pk_fma_f32 v[32:33], v[70:71], v[32:33], v[116:117] op_sel_hi:[1,0,1] neg_lo:[0,0,1] neg_hi:[0,0,1]
	v_pk_mul_f32 v[38:39], v[10:11], v[28:29] op_sel:[0,1] op_sel_hi:[0,0] neg_lo:[1,1] neg_hi:[1,0]
	v_pk_fma_f32 v[86:87], v[28:29], v[10:11], v[38:39] op_sel_hi:[1,0,1] neg_lo:[0,1,0] neg_hi:[0,1,0]
	v_pk_add_f32 v[28:29], v[44:45], v[24:25]
	v_pk_add_f32 v[24:25], v[44:45], v[24:25] neg_lo:[0,1] neg_hi:[0,1]
	v_pk_mul_f32 v[70:71], v[32:33], v[124:125] op_sel:[1,0] op_sel_hi:[0,0] neg_lo:[1,1] neg_hi:[0,1]
	v_pk_fma_f32 v[70:71], v[118:119], v[32:33], v[70:71] op_sel_hi:[0,1,1] neg_lo:[1,0,0] neg_hi:[1,0,0]
	v_pk_add_f32 v[32:33], v[126:127], v[48:49]
	v_pk_mul_f32 v[38:39], v[34:35], v[24:25] op_sel:[0,1] op_sel_hi:[0,0] neg_lo:[1,1] neg_hi:[1,0]
	v_pk_fma_f32 v[88:89], v[30:31], v[24:25], v[38:39] op_sel_hi:[0,1,1] neg_lo:[1,0,0] neg_hi:[1,0,0]
	v_pk_add_f32 v[24:25], v[32:33], v[20:21]
	v_pk_add_f32 v[32:33], v[32:33], v[20:21] neg_lo:[0,1] neg_hi:[0,1]
	v_pk_add_f32 v[20:21], v[84:85], v[22:23]
	v_pk_add_f32 v[22:23], v[84:85], v[22:23] neg_lo:[0,1] neg_hi:[0,1]
	v_pk_add_f32 v[48:49], v[126:127], v[48:49] neg_lo:[0,1] neg_hi:[0,1]
	v_pk_mul_f32 v[38:39], v[10:11], v[22:23] op_sel:[0,1] op_sel_hi:[0,0] neg_lo:[1,1] neg_hi:[1,0]
	v_pk_fma_f32 v[22:23], v[22:23], v[10:11], v[38:39] op_sel_hi:[1,0,1]
	v_pk_add_f32 v[38:39], v[16:17], v[42:43]
	v_pk_add_f32 v[16:17], v[16:17], v[42:43] neg_lo:[0,1] neg_hi:[0,1]
	s_nop 0
	v_xor_b32_e32 v43, 0x80000000, v16
	v_mov_b32_e32 v42, v17
	v_pk_add_f32 v[16:17], v[78:79], v[28:29]
	v_pk_add_f32 v[28:29], v[78:79], v[28:29] neg_lo:[0,1] neg_hi:[0,1]
	s_nop 0
	v_pk_mul_f32 v[44:45], v[10:11], v[28:29] op_sel:[0,1] op_sel_hi:[0,0] neg_lo:[1,1] neg_hi:[1,0]
	v_pk_fma_f32 v[78:79], v[10:11], v[28:29], v[44:45] op_sel_hi:[0,1,1] neg_lo:[1,0,0] neg_hi:[1,0,0]
	v_pk_add_f32 v[28:29], v[24:25], v[38:39]
	v_pk_add_f32 v[24:25], v[24:25], v[38:39] neg_lo:[0,1] neg_hi:[0,1]
	v_pk_add_f32 v[38:39], v[20:21], v[16:17]
	v_pk_add_f32 v[16:17], v[20:21], v[16:17] neg_lo:[0,1] neg_hi:[0,1]
	v_pk_add_f32 v[84:85], v[28:29], v[38:39]
	v_pk_add_f32 v[44:45], v[24:25], v[16:17] op_sel:[0,1] op_sel_hi:[1,0] neg_hi:[0,1]
	v_pk_add_f32 v[20:21], v[24:25], v[16:17] op_sel:[0,1] op_sel_hi:[1,0] neg_lo:[0,1]
	v_pk_add_f32 v[24:25], v[22:23], v[78:79]
	v_pk_add_f32 v[22:23], v[22:23], v[78:79] neg_lo:[0,1] neg_hi:[0,1]
	v_pk_add_f32 v[16:17], v[32:33], v[42:43]
	v_pk_add_f32 v[32:33], v[32:33], v[42:43] neg_lo:[0,1] neg_hi:[0,1]
	v_pk_add_f32 v[28:29], v[28:29], v[38:39] neg_lo:[0,1] neg_hi:[0,1]
	v_pk_add_f32 v[78:79], v[16:17], v[24:25]
	v_pk_add_f32 v[24:25], v[16:17], v[24:25] neg_lo:[0,1] neg_hi:[0,1]
	v_pk_add_f32 v[38:39], v[32:33], v[22:23] op_sel:[0,1] op_sel_hi:[1,0] neg_hi:[0,1]
	v_pk_add_f32 v[16:17], v[32:33], v[22:23] op_sel:[0,1] op_sel_hi:[1,0] neg_lo:[0,1]
	v_pk_add_f32 v[32:33], v[56:57], v[26:27]
	v_pk_add_f32 v[26:27], v[56:57], v[26:27] neg_lo:[0,1] neg_hi:[0,1]
	v_pk_add_f32 v[22:23], v[48:49], v[80:81]
	v_pk_add_f32 v[42:43], v[48:49], v[80:81] neg_lo:[0,1] neg_hi:[0,1]
	v_pk_mul_f32 v[48:49], v[10:11], v[26:27] op_sel:[0,1] op_sel_hi:[0,0] neg_lo:[1,1] neg_hi:[1,0]
	v_pk_fma_f32 v[26:27], v[10:11], v[26:27], v[48:49] op_sel_hi:[0,1,1]
	v_pk_add_f32 v[48:49], v[18:19], v[86:87]
	v_pk_add_f32 v[18:19], v[18:19], v[86:87] neg_lo:[0,1] neg_hi:[0,1]
	v_pk_add_f32 v[80:81], v[82:83], v[88:89] neg_lo:[0,1] neg_hi:[0,1]
	v_xor_b32_e32 v57, 0x80000000, v18
	v_mov_b32_e32 v56, v19
	v_pk_add_f32 v[18:19], v[82:83], v[88:89]
	v_pk_mul_f32 v[82:83], v[10:11], v[80:81] op_sel:[0,1] op_sel_hi:[0,0] neg_lo:[1,1] neg_hi:[1,0]
	v_pk_fma_f32 v[80:81], v[10:11], v[80:81], v[82:83] op_sel_hi:[0,1,1] neg_lo:[1,0,0] neg_hi:[1,0,0]
	v_pk_add_f32 v[82:83], v[22:23], v[48:49]
	v_pk_add_f32 v[22:23], v[22:23], v[48:49] neg_lo:[0,1] neg_hi:[0,1]
	v_pk_add_f32 v[48:49], v[32:33], v[18:19]
	v_pk_add_f32 v[18:19], v[32:33], v[18:19] neg_lo:[0,1] neg_hi:[0,1]
	v_pk_add_f32 v[88:89], v[82:83], v[48:49]
	v_xor_b32_e32 v87, 0x80000000, v18
	v_mov_b32_e32 v86, v19
	v_pk_add_f32 v[18:19], v[42:43], v[56:57]
	v_pk_add_f32 v[56:57], v[42:43], v[56:57] neg_lo:[0,1] neg_hi:[0,1]
	v_pk_add_f32 v[42:43], v[26:27], v[80:81]
	v_pk_add_f32 v[26:27], v[26:27], v[80:81] neg_lo:[0,1] neg_hi:[0,1]
	v_pk_add_f32 v[32:33], v[82:83], v[48:49] neg_lo:[0,1] neg_hi:[0,1]
	v_xor_b32_e32 v81, 0x80000000, v26
	v_mov_b32_e32 v80, v27
	v_pk_add_f32 v[82:83], v[18:19], v[42:43]
	v_pk_add_f32 v[26:27], v[18:19], v[42:43] neg_lo:[0,1] neg_hi:[0,1]
	v_pk_add_f32 v[42:43], v[56:57], v[80:81]
	v_pk_add_f32 v[18:19], v[56:57], v[80:81] neg_lo:[0,1] neg_hi:[0,1]
	v_pk_add_f32 v[56:57], v[36:37], v[76:77]
	v_pk_add_f32 v[76:77], v[36:37], v[76:77] neg_lo:[0,1] neg_hi:[0,1]
	v_pk_add_f32 v[36:37], v[40:41], v[60:61]
	v_pk_add_f32 v[40:41], v[40:41], v[60:61] neg_lo:[0,1] neg_hi:[0,1]
	v_pk_add_f32 v[48:49], v[22:23], v[86:87]
	v_pk_mul_f32 v[60:61], v[34:35], v[40:41] op_sel:[0,1] op_sel_hi:[0,0] neg_lo:[1,1] neg_hi:[1,0]
	v_pk_fma_f32 v[40:41], v[30:31], v[40:41], v[60:61] op_sel_hi:[0,1,1]
	v_pk_add_f32 v[60:61], v[46:47], v[62:63]
	v_pk_add_f32 v[46:47], v[46:47], v[62:63] neg_lo:[0,1] neg_hi:[0,1]
	v_pk_add_f32 v[22:23], v[22:23], v[86:87] neg_lo:[0,1] neg_hi:[0,1]
	v_pk_mul_f32 v[62:63], v[10:11], v[46:47] op_sel:[0,1] op_sel_hi:[0,0] neg_lo:[1,1] neg_hi:[1,0]
	v_pk_fma_f32 v[62:63], v[10:11], v[46:47], v[62:63] op_sel_hi:[0,1,1]
	v_pk_add_f32 v[46:47], v[50:51], v[58:59]
	v_pk_add_f32 v[50:51], v[50:51], v[58:59] neg_lo:[0,1] neg_hi:[0,1]
	s_nop 0
	v_pk_mul_f32 v[58:59], v[30:31], v[50:51] op_sel:[0,1] op_sel_hi:[0,0] neg_lo:[1,1] neg_hi:[1,0]
	v_pk_fma_f32 v[50:51], v[34:35], v[50:51], v[58:59] op_sel_hi:[0,1,1]
	v_pk_add_f32 v[58:59], v[52:53], v[74:75]
	v_pk_add_f32 v[52:53], v[52:53], v[74:75] neg_lo:[0,1] neg_hi:[0,1]
	s_nop 0
	v_xor_b32_e32 v75, 0x80000000, v52
	v_mov_b32_e32 v74, v53
	v_pk_add_f32 v[52:53], v[64:65], v[72:73]
	v_pk_add_f32 v[64:65], v[64:65], v[72:73] neg_lo:[0,1] neg_hi:[0,1]
	s_nop 0
	v_pk_mul_f32 v[72:73], v[30:31], v[64:65] op_sel:[0,1] op_sel_hi:[0,0] neg_lo:[1,1] neg_hi:[1,0]
	v_pk_fma_f32 v[64:65], v[34:35], v[64:65], v[72:73] op_sel_hi:[0,1,1] neg_lo:[1,0,0] neg_hi:[1,0,0]
	v_pk_add_f32 v[72:73], v[66:67], v[68:69]
	v_pk_add_f32 v[66:67], v[66:67], v[68:69] neg_lo:[0,1] neg_hi:[0,1]
	s_nop 0
	v_pk_mul_f32 v[68:69], v[10:11], v[66:67] op_sel:[0,1] op_sel_hi:[0,0] neg_lo:[1,1] neg_hi:[1,0]
	v_pk_fma_f32 v[66:67], v[10:11], v[66:67], v[68:69] op_sel_hi:[0,1,1] neg_lo:[1,0,0] neg_hi:[1,0,0]
	v_pk_add_f32 v[68:69], v[54:55], v[70:71]
	v_pk_add_f32 v[54:55], v[54:55], v[70:71] neg_lo:[0,1] neg_hi:[0,1]
	s_nop 0
	v_pk_mul_f32 v[34:35], v[34:35], v[54:55] op_sel:[0,1] op_sel_hi:[0,0] neg_lo:[1,1] neg_hi:[1,0]
	v_pk_fma_f32 v[34:35], v[30:31], v[54:55], v[34:35] op_sel_hi:[0,1,1] neg_lo:[1,0,0] neg_hi:[1,0,0]
	v_pk_add_f32 v[30:31], v[56:57], v[58:59]
	v_pk_add_f32 v[54:55], v[56:57], v[58:59] neg_lo:[0,1] neg_hi:[0,1]
	v_pk_add_f32 v[56:57], v[52:53], v[36:37]
	v_pk_add_f32 v[36:37], v[36:37], v[52:53] neg_lo:[0,1] neg_hi:[0,1]
	s_nop 0
	v_pk_mul_f32 v[52:53], v[10:11], v[36:37] op_sel:[0,1] op_sel_hi:[0,0] neg_lo:[1,1] neg_hi:[1,0]
	v_pk_fma_f32 v[58:59], v[10:11], v[36:37], v[52:53] op_sel_hi:[0,1,1]
	v_pk_add_f32 v[52:53], v[60:61], v[72:73] neg_lo:[0,1] neg_hi:[0,1]
	v_pk_add_f32 v[36:37], v[60:61], v[72:73]
	v_xor_b32_e32 v61, 0x80000000, v52
	v_mov_b32_e32 v60, v53
	v_pk_add_f32 v[52:53], v[46:47], v[68:69]
	v_pk_add_f32 v[46:47], v[46:47], v[68:69] neg_lo:[0,1] neg_hi:[0,1]
	v_pk_add_f32 v[72:73], v[64:65], v[40:41]
	v_pk_add_f32 v[40:41], v[40:41], v[64:65] neg_lo:[0,1] neg_hi:[0,1]
	v_pk_mul_f32 v[68:69], v[10:11], v[46:47] op_sel:[0,1] op_sel_hi:[0,0] neg_lo:[1,1] neg_hi:[1,0]
	v_pk_fma_f32 v[46:47], v[10:11], v[46:47], v[68:69] op_sel_hi:[0,1,1] neg_lo:[1,0,0] neg_hi:[1,0,0]
	v_pk_add_f32 v[68:69], v[30:31], v[36:37]
	v_pk_add_f32 v[30:31], v[30:31], v[36:37] neg_lo:[0,1] neg_hi:[0,1]
	v_pk_add_f32 v[36:37], v[56:57], v[52:53]
	v_pk_add_f32 v[52:53], v[56:57], v[52:53] neg_lo:[0,1] neg_hi:[0,1]
	v_pk_mul_f32 v[64:65], v[10:11], v[40:41] op_sel:[0,1] op_sel_hi:[0,0] neg_lo:[1,1] neg_hi:[1,0]
	v_xor_b32_e32 v57, 0x80000000, v52
	v_mov_b32_e32 v56, v53
	v_pk_fma_f32 v[64:65], v[10:11], v[40:41], v[64:65] op_sel_hi:[0,1,1]
	v_pk_add_f32 v[40:41], v[62:63], v[66:67]
	v_pk_add_f32 v[62:63], v[62:63], v[66:67] neg_lo:[0,1] neg_hi:[0,1]
	v_pk_add_f32 v[70:71], v[68:69], v[36:37]
	v_pk_add_f32 v[52:53], v[68:69], v[36:37] neg_lo:[0,1] neg_hi:[0,1]
	v_pk_add_f32 v[68:69], v[30:31], v[56:57]
	v_pk_add_f32 v[36:37], v[30:31], v[56:57] neg_lo:[0,1] neg_hi:[0,1]
	v_pk_add_f32 v[56:57], v[58:59], v[46:47]
	v_pk_add_f32 v[46:47], v[58:59], v[46:47] neg_lo:[0,1] neg_hi:[0,1]
	v_xor_b32_e32 v67, 0x80000000, v62
	v_mov_b32_e32 v66, v63
	v_pk_add_f32 v[62:63], v[50:51], v[34:35]
	v_pk_add_f32 v[34:35], v[50:51], v[34:35] neg_lo:[0,1] neg_hi:[0,1]
	v_pk_add_f32 v[30:31], v[54:55], v[60:61]
	v_pk_add_f32 v[54:55], v[54:55], v[60:61] neg_lo:[0,1] neg_hi:[0,1]
	v_xor_b32_e32 v59, 0x80000000, v46
	v_mov_b32_e32 v58, v47
	v_pk_add_f32 v[60:61], v[30:31], v[56:57]
	v_pk_add_f32 v[46:47], v[30:31], v[56:57] neg_lo:[0,1] neg_hi:[0,1]
	v_pk_add_f32 v[56:57], v[54:55], v[58:59]
	v_pk_add_f32 v[30:31], v[54:55], v[58:59] neg_lo:[0,1] neg_hi:[0,1]
	v_pk_add_f32 v[54:55], v[76:77], v[74:75]
	v_pk_mul_f32 v[50:51], v[10:11], v[34:35] op_sel:[0,1] op_sel_hi:[0,0] neg_lo:[1,1] neg_hi:[1,0]
	v_pk_add_f32 v[58:59], v[76:77], v[74:75] neg_lo:[0,1] neg_hi:[0,1]
	v_pk_fma_f32 v[34:35], v[10:11], v[34:35], v[50:51] op_sel_hi:[0,1,1] neg_lo:[1,0,0] neg_hi:[1,0,0]
	v_pk_add_f32 v[50:51], v[54:55], v[40:41]
	v_pk_add_f32 v[40:41], v[54:55], v[40:41] neg_lo:[0,1] neg_hi:[0,1]
	v_pk_add_f32 v[54:55], v[72:73], v[62:63]
	v_pk_add_f32 v[62:63], v[72:73], v[62:63] neg_lo:[0,1] neg_hi:[0,1]
	v_lshl_add_u32 v10, v13, 3, 0
	v_xor_b32_e32 v73, 0x80000000, v62
	v_mov_b32_e32 v72, v63
	v_pk_add_f32 v[62:63], v[50:51], v[54:55]
	v_pk_add_f32 v[54:55], v[50:51], v[54:55] neg_lo:[0,1] neg_hi:[0,1]
	v_pk_add_f32 v[50:51], v[58:59], v[66:67]
	v_pk_add_f32 v[58:59], v[58:59], v[66:67] neg_lo:[0,1] neg_hi:[0,1]
	v_pk_add_f32 v[66:67], v[64:65], v[34:35]
	v_pk_add_f32 v[34:35], v[64:65], v[34:35] neg_lo:[0,1] neg_hi:[0,1]
	v_pk_add_f32 v[74:75], v[40:41], v[72:73]
	v_pk_add_f32 v[40:41], v[40:41], v[72:73] neg_lo:[0,1] neg_hi:[0,1]
	v_pk_add_f32 v[72:73], v[50:51], v[66:67]
	v_pk_add_f32 v[50:51], v[50:51], v[66:67] neg_lo:[0,1] neg_hi:[0,1]
	v_pk_add_f32 v[66:67], v[58:59], v[34:35] op_sel:[0,1] op_sel_hi:[1,0] neg_hi:[0,1]
	v_pk_add_f32 v[34:35], v[58:59], v[34:35] op_sel:[0,1] op_sel_hi:[1,0] neg_lo:[0,1]
	v_pk_mul_f32 v[58:59], v[84:85], s[14:15] op_sel:[1,0] neg_lo:[1,0]
	s_nop 0
	v_pk_fma_f32 v[58:59], v[84:85], s[94:95], v[58:59] op_sel_hi:[0,1,1]
	ds_write_b64 v10, v[58:59]
	v_pk_fma_f32 v[58:59], v[178:179], s[90:91], v[178:179] op_sel:[1,0,0] op_sel_hi:[0,1,1]
	v_pk_mul_f32 v[64:65], v[58:59], v[70:71] op_sel:[1,1] op_sel_hi:[0,1] neg_lo:[0,1]
	v_pk_fma_f32 v[64:65], v[58:59], v[70:71], v[64:65] op_sel_hi:[1,0,1]
	ds_write_b64 v10, v[64:65] offset:4224
	v_pk_mul_f32 v[64:65], v[178:179], v[58:59] op_sel:[1,1] op_sel_hi:[0,1] neg_lo:[0,1]
	v_pk_fma_f32 v[58:59], v[178:179], v[58:59], v[64:65] op_sel_hi:[1,0,1]
	s_nop 0
	v_pk_mul_f32 v[64:65], v[58:59], v[88:89] op_sel:[1,1] op_sel_hi:[0,1] neg_lo:[0,1]
	v_pk_fma_f32 v[64:65], v[58:59], v[88:89], v[64:65] op_sel_hi:[1,0,1]
	ds_write_b64 v10, v[64:65] offset:8448
	v_pk_mul_f32 v[64:65], v[178:179], v[58:59] op_sel:[1,1] op_sel_hi:[0,1] neg_lo:[0,1]
	v_pk_fma_f32 v[58:59], v[178:179], v[58:59], v[64:65] op_sel_hi:[1,0,1]
	s_nop 0
	v_pk_mul_f32 v[64:65], v[58:59], v[62:63] op_sel:[1,1] op_sel_hi:[0,1] neg_lo:[0,1]
	v_pk_fma_f32 v[62:63], v[58:59], v[62:63], v[64:65] op_sel_hi:[1,0,1]
	ds_write_b64 v10, v[62:63] offset:12672
	v_pk_mul_f32 v[62:63], v[178:179], v[58:59] op_sel:[1,1] op_sel_hi:[0,1] neg_lo:[0,1]
	v_pk_fma_f32 v[58:59], v[178:179], v[58:59], v[62:63] op_sel_hi:[1,0,1]
	s_nop 0
	v_pk_mul_f32 v[62:63], v[58:59], v[78:79] op_sel:[1,1] op_sel_hi:[0,1] neg_lo:[0,1]
	v_pk_fma_f32 v[62:63], v[58:59], v[78:79], v[62:63] op_sel_hi:[1,0,1]
	ds_write_b64 v10, v[62:63] offset:16896
	v_pk_mul_f32 v[62:63], v[178:179], v[58:59] op_sel:[1,1] op_sel_hi:[0,1] neg_lo:[0,1]
	v_pk_fma_f32 v[58:59], v[178:179], v[58:59], v[62:63] op_sel_hi:[1,0,1]
	s_nop 0
	v_pk_mul_f32 v[62:63], v[58:59], v[60:61] op_sel:[1,1] op_sel_hi:[0,1] neg_lo:[0,1]
	v_pk_fma_f32 v[60:61], v[58:59], v[60:61], v[62:63] op_sel_hi:[1,0,1]
	ds_write_b64 v10, v[60:61] offset:21120
	v_pk_mul_f32 v[60:61], v[178:179], v[58:59] op_sel:[1,1] op_sel_hi:[0,1] neg_lo:[0,1]
	v_pk_fma_f32 v[58:59], v[178:179], v[58:59], v[60:61] op_sel_hi:[1,0,1]
	s_nop 0
	v_pk_mul_f32 v[60:61], v[82:83], v[58:59] op_sel:[1,1] op_sel_hi:[1,0] neg_lo:[1,0]
	s_nop 0
	v_pk_fma_f32 v[60:61], v[82:83], v[58:59], v[60:61] op_sel_hi:[0,1,1]
	ds_write_b64 v10, v[60:61] offset:25344
	v_pk_mul_f32 v[60:61], v[178:179], v[58:59] op_sel:[1,1] op_sel_hi:[0,1] neg_lo:[0,1]
	v_pk_fma_f32 v[58:59], v[178:179], v[58:59], v[60:61] op_sel_hi:[1,0,1]
	s_nop 0
	v_pk_mul_f32 v[60:61], v[72:73], v[58:59] op_sel:[1,1] op_sel_hi:[1,0] neg_lo:[1,0]
	s_nop 0
	v_pk_fma_f32 v[60:61], v[72:73], v[58:59], v[60:61] op_sel_hi:[0,1,1]
	ds_write_b64 v10, v[60:61] offset:29568
	v_pk_mul_f32 v[60:61], v[178:179], v[58:59] op_sel:[1,1] op_sel_hi:[0,1] neg_lo:[0,1]
	v_pk_fma_f32 v[58:59], v[178:179], v[58:59], v[60:61] op_sel_hi:[1,0,1]
	s_nop 0
	v_pk_mul_f32 v[60:61], v[44:45], v[58:59] op_sel:[1,1] op_sel_hi:[1,0] neg_lo:[1,0]
	s_nop 0
	v_pk_fma_f32 v[44:45], v[44:45], v[58:59], v[60:61] op_sel_hi:[0,1,1]
	ds_write_b64 v10, v[44:45] offset:33792
	v_pk_mul_f32 v[44:45], v[178:179], v[58:59] op_sel:[1,1] op_sel_hi:[0,1] neg_lo:[0,1]
	v_pk_fma_f32 v[44:45], v[178:179], v[58:59], v[44:45] op_sel_hi:[1,0,1]
	s_nop 0
	v_pk_mul_f32 v[58:59], v[68:69], v[44:45] op_sel:[1,1] op_sel_hi:[1,0] neg_lo:[1,0]
	s_nop 0
	v_pk_fma_f32 v[58:59], v[68:69], v[44:45], v[58:59] op_sel_hi:[0,1,1]
	ds_write_b64 v10, v[58:59] offset:38016
	v_pk_mul_f32 v[58:59], v[178:179], v[44:45] op_sel:[1,1] op_sel_hi:[0,1] neg_lo:[0,1]
	v_pk_fma_f32 v[44:45], v[178:179], v[44:45], v[58:59] op_sel_hi:[1,0,1]
	s_nop 0
	v_pk_mul_f32 v[58:59], v[48:49], v[44:45] op_sel:[1,1] op_sel_hi:[1,0] neg_lo:[1,0]
	s_nop 0
	v_pk_fma_f32 v[48:49], v[48:49], v[44:45], v[58:59] op_sel_hi:[0,1,1]
	ds_write_b64 v10, v[48:49] offset:42240
	v_pk_mul_f32 v[48:49], v[178:179], v[44:45] op_sel:[1,1] op_sel_hi:[0,1] neg_lo:[0,1]
	v_pk_fma_f32 v[44:45], v[178:179], v[44:45], v[48:49] op_sel_hi:[1,0,1]
	s_nop 0
	v_pk_mul_f32 v[48:49], v[74:75], v[44:45] op_sel:[1,1] op_sel_hi:[1,0] neg_lo:[1,0]
	s_nop 0
	v_pk_fma_f32 v[48:49], v[74:75], v[44:45], v[48:49] op_sel_hi:[0,1,1]
	ds_write_b64 v10, v[48:49] offset:46464
	v_pk_mul_f32 v[48:49], v[178:179], v[44:45] op_sel:[1,1] op_sel_hi:[0,1] neg_lo:[0,1]
	v_pk_fma_f32 v[44:45], v[178:179], v[44:45], v[48:49] op_sel_hi:[1,0,1]
	s_nop 0
	v_pk_mul_f32 v[48:49], v[38:39], v[44:45] op_sel:[1,1] op_sel_hi:[1,0] neg_lo:[1,0]
	s_nop 0
	v_pk_fma_f32 v[38:39], v[38:39], v[44:45], v[48:49] op_sel_hi:[0,1,1]
	ds_write_b64 v10, v[38:39] offset:50688
	v_pk_mul_f32 v[38:39], v[178:179], v[44:45] op_sel:[1,1] op_sel_hi:[0,1] neg_lo:[0,1]
	v_pk_fma_f32 v[38:39], v[178:179], v[44:45], v[38:39] op_sel_hi:[1,0,1]
	s_nop 0
	v_pk_mul_f32 v[44:45], v[56:57], v[38:39] op_sel:[1,1] op_sel_hi:[1,0] neg_lo:[1,0]
	s_nop 0
	v_pk_fma_f32 v[44:45], v[56:57], v[38:39], v[44:45] op_sel_hi:[0,1,1]
	ds_write_b64 v10, v[44:45] offset:54912
	v_pk_mul_f32 v[44:45], v[178:179], v[38:39] op_sel:[1,1] op_sel_hi:[0,1] neg_lo:[0,1]
	v_pk_fma_f32 v[38:39], v[178:179], v[38:39], v[44:45] op_sel_hi:[1,0,1]
	s_nop 0
	v_pk_mul_f32 v[44:45], v[42:43], v[38:39] op_sel:[1,1] op_sel_hi:[1,0] neg_lo:[1,0]
	s_nop 0
	v_pk_fma_f32 v[42:43], v[42:43], v[38:39], v[44:45] op_sel_hi:[0,1,1]
	ds_write_b64 v10, v[42:43] offset:59136
	v_pk_mul_f32 v[42:43], v[178:179], v[38:39] op_sel:[1,1] op_sel_hi:[0,1] neg_lo:[0,1]
	v_pk_fma_f32 v[38:39], v[178:179], v[38:39], v[42:43] op_sel_hi:[1,0,1]
	s_nop 0
	v_pk_mul_f32 v[42:43], v[66:67], v[38:39] op_sel:[1,1] op_sel_hi:[1,0] neg_lo:[1,0]
	s_nop 0
	v_pk_fma_f32 v[42:43], v[66:67], v[38:39], v[42:43] op_sel_hi:[0,1,1]
	ds_write_b64 v10, v[42:43] offset:63360
	v_pk_mul_f32 v[42:43], v[178:179], v[38:39] op_sel:[1,1] op_sel_hi:[0,1] neg_lo:[0,1]
	v_pk_fma_f32 v[38:39], v[178:179], v[38:39], v[42:43] op_sel_hi:[1,0,1]
	s_nop 0
	v_pk_mul_f32 v[42:43], v[28:29], v[38:39] op_sel:[1,1] op_sel_hi:[1,0] neg_lo:[1,0]
	v_add_u32_e32 v13, 0x10800, v10
	v_pk_fma_f32 v[28:29], v[28:29], v[38:39], v[42:43] op_sel_hi:[0,1,1]
	ds_write_b64 v13, v[28:29]
	v_pk_mul_f32 v[28:29], v[178:179], v[38:39] op_sel:[1,1] op_sel_hi:[0,1] neg_lo:[0,1]
	v_pk_fma_f32 v[28:29], v[178:179], v[38:39], v[28:29] op_sel_hi:[1,0,1]
	s_nop 0
	v_pk_mul_f32 v[38:39], v[52:53], v[28:29] op_sel:[1,1] op_sel_hi:[1,0] neg_lo:[1,0]
	v_add_u32_e32 v13, 0x11880, v10
	v_pk_fma_f32 v[38:39], v[52:53], v[28:29], v[38:39] op_sel_hi:[0,1,1]
	ds_write_b64 v13, v[38:39]
	v_pk_mul_f32 v[38:39], v[178:179], v[28:29] op_sel:[1,1] op_sel_hi:[0,1] neg_lo:[0,1]
	v_pk_fma_f32 v[28:29], v[178:179], v[28:29], v[38:39] op_sel_hi:[1,0,1]
	s_nop 0
	v_pk_mul_f32 v[38:39], v[32:33], v[28:29] op_sel:[1,1] op_sel_hi:[1,0] neg_lo:[1,0]
	v_add_u32_e32 v13, 0x12900, v10
	v_pk_fma_f32 v[32:33], v[32:33], v[28:29], v[38:39] op_sel_hi:[0,1,1]
	ds_write_b64 v13, v[32:33]
	v_pk_mul_f32 v[32:33], v[178:179], v[28:29] op_sel:[1,1] op_sel_hi:[0,1] neg_lo:[0,1]
	v_pk_fma_f32 v[28:29], v[178:179], v[28:29], v[32:33] op_sel_hi:[1,0,1]
	s_nop 0
	v_pk_mul_f32 v[32:33], v[54:55], v[28:29] op_sel:[1,1] op_sel_hi:[1,0] neg_lo:[1,0]
	v_add_u32_e32 v13, 0x13980, v10
	v_pk_fma_f32 v[32:33], v[54:55], v[28:29], v[32:33] op_sel_hi:[0,1,1]
	ds_write_b64 v13, v[32:33]
	v_pk_mul_f32 v[32:33], v[178:179], v[28:29] op_sel:[1,1] op_sel_hi:[0,1] neg_lo:[0,1]
	v_pk_fma_f32 v[28:29], v[178:179], v[28:29], v[32:33] op_sel_hi:[1,0,1]
	s_nop 0
	v_pk_mul_f32 v[32:33], v[24:25], v[28:29] op_sel:[1,1] op_sel_hi:[1,0] neg_lo:[1,0]
	v_add_u32_e32 v13, 0x14a00, v10
	v_pk_fma_f32 v[24:25], v[24:25], v[28:29], v[32:33] op_sel_hi:[0,1,1]
	ds_write_b64 v13, v[24:25]
	v_pk_mul_f32 v[24:25], v[178:179], v[28:29] op_sel:[1,1] op_sel_hi:[0,1] neg_lo:[0,1]
	v_pk_fma_f32 v[24:25], v[178:179], v[28:29], v[24:25] op_sel_hi:[1,0,1]
	s_nop 0
	v_pk_mul_f32 v[28:29], v[46:47], v[24:25] op_sel:[1,1] op_sel_hi:[1,0] neg_lo:[1,0]
	v_add_u32_e32 v13, 0x15a80, v10
	v_pk_fma_f32 v[28:29], v[46:47], v[24:25], v[28:29] op_sel_hi:[0,1,1]
	ds_write_b64 v13, v[28:29]
	v_pk_mul_f32 v[28:29], v[178:179], v[24:25] op_sel:[1,1] op_sel_hi:[0,1] neg_lo:[0,1]
	v_pk_fma_f32 v[24:25], v[178:179], v[24:25], v[28:29] op_sel_hi:[1,0,1]
	s_nop 0
	v_pk_mul_f32 v[28:29], v[26:27], v[24:25] op_sel:[1,1] op_sel_hi:[1,0] neg_lo:[1,0]
	v_add_u32_e32 v13, 0x16b00, v10
	v_pk_fma_f32 v[26:27], v[26:27], v[24:25], v[28:29] op_sel_hi:[0,1,1]
	ds_write_b64 v13, v[26:27]
	v_pk_mul_f32 v[26:27], v[178:179], v[24:25] op_sel:[1,1] op_sel_hi:[0,1] neg_lo:[0,1]
	v_pk_fma_f32 v[24:25], v[178:179], v[24:25], v[26:27] op_sel_hi:[1,0,1]
	s_nop 0
	v_pk_mul_f32 v[26:27], v[50:51], v[24:25] op_sel:[1,1] op_sel_hi:[1,0] neg_lo:[1,0]
	v_add_u32_e32 v13, 0x17b80, v10
	v_pk_fma_f32 v[26:27], v[50:51], v[24:25], v[26:27] op_sel_hi:[0,1,1]
	ds_write_b64 v13, v[26:27]
	v_pk_mul_f32 v[26:27], v[178:179], v[24:25] op_sel:[1,1] op_sel_hi:[0,1] neg_lo:[0,1]
	v_pk_fma_f32 v[24:25], v[178:179], v[24:25], v[26:27] op_sel_hi:[1,0,1]
	s_nop 0
	v_pk_mul_f32 v[26:27], v[20:21], v[24:25] op_sel:[1,1] op_sel_hi:[1,0] neg_lo:[1,0]
	v_add_u32_e32 v13, 0x18c00, v10
	v_pk_fma_f32 v[20:21], v[20:21], v[24:25], v[26:27] op_sel_hi:[0,1,1]
	ds_write_b64 v13, v[20:21]
	v_pk_mul_f32 v[20:21], v[178:179], v[24:25] op_sel:[1,1] op_sel_hi:[0,1] neg_lo:[0,1]
	v_pk_fma_f32 v[20:21], v[178:179], v[24:25], v[20:21] op_sel_hi:[1,0,1]
	s_nop 0
	v_pk_mul_f32 v[24:25], v[36:37], v[20:21] op_sel:[1,1] op_sel_hi:[1,0] neg_lo:[1,0]
	v_add_u32_e32 v13, 0x19c80, v10
	v_pk_fma_f32 v[24:25], v[36:37], v[20:21], v[24:25] op_sel_hi:[0,1,1]
	ds_write_b64 v13, v[24:25]
	v_pk_mul_f32 v[24:25], v[178:179], v[20:21] op_sel:[1,1] op_sel_hi:[0,1] neg_lo:[0,1]
	v_pk_fma_f32 v[20:21], v[178:179], v[20:21], v[24:25] op_sel_hi:[1,0,1]
	s_nop 0
	v_pk_mul_f32 v[24:25], v[22:23], v[20:21] op_sel:[1,1] op_sel_hi:[1,0] neg_lo:[1,0]
	v_add_u32_e32 v13, 0x1ad00, v10
	v_pk_fma_f32 v[22:23], v[22:23], v[20:21], v[24:25] op_sel_hi:[0,1,1]
	ds_write_b64 v13, v[22:23]
	v_pk_mul_f32 v[22:23], v[178:179], v[20:21] op_sel:[1,1] op_sel_hi:[0,1] neg_lo:[0,1]
	v_pk_fma_f32 v[20:21], v[178:179], v[20:21], v[22:23] op_sel_hi:[1,0,1]
	s_nop 0
	v_pk_mul_f32 v[22:23], v[40:41], v[20:21] op_sel:[1,1] op_sel_hi:[1,0] neg_lo:[1,0]
	v_add_u32_e32 v13, 0x1bd80, v10
	v_pk_fma_f32 v[22:23], v[40:41], v[20:21], v[22:23] op_sel_hi:[0,1,1]
	ds_write_b64 v13, v[22:23]
	v_pk_mul_f32 v[22:23], v[178:179], v[20:21] op_sel:[1,1] op_sel_hi:[0,1] neg_lo:[0,1]
	v_pk_fma_f32 v[20:21], v[178:179], v[20:21], v[22:23] op_sel_hi:[1,0,1]
	s_nop 0
	v_pk_mul_f32 v[22:23], v[16:17], v[20:21] op_sel:[1,1] op_sel_hi:[1,0] neg_lo:[1,0]
	v_add_u32_e32 v13, 0x1ce00, v10
	v_pk_fma_f32 v[16:17], v[16:17], v[20:21], v[22:23] op_sel_hi:[0,1,1]
	ds_write_b64 v13, v[16:17]
	v_pk_mul_f32 v[16:17], v[178:179], v[20:21] op_sel:[1,1] op_sel_hi:[0,1] neg_lo:[0,1]
	v_pk_fma_f32 v[16:17], v[178:179], v[20:21], v[16:17] op_sel_hi:[1,0,1]
	s_nop 0
	v_pk_mul_f32 v[20:21], v[30:31], v[16:17] op_sel:[1,1] op_sel_hi:[1,0] neg_lo:[1,0]
	v_add_u32_e32 v13, 0x1de80, v10
	v_pk_fma_f32 v[20:21], v[30:31], v[16:17], v[20:21] op_sel_hi:[0,1,1]
	ds_write_b64 v13, v[20:21]
	v_pk_mul_f32 v[20:21], v[178:179], v[16:17] op_sel:[1,1] op_sel_hi:[0,1] neg_lo:[0,1]
	v_pk_fma_f32 v[16:17], v[178:179], v[16:17], v[20:21] op_sel_hi:[1,0,1]
	s_nop 0
	v_pk_mul_f32 v[20:21], v[18:19], v[16:17] op_sel:[1,1] op_sel_hi:[1,0] neg_lo:[1,0]
	v_add_u32_e32 v13, 0x1ef00, v10
	v_pk_fma_f32 v[18:19], v[18:19], v[16:17], v[20:21] op_sel_hi:[0,1,1]
	ds_write_b64 v13, v[18:19]
	v_pk_mul_f32 v[18:19], v[178:179], v[16:17] op_sel:[1,1] op_sel_hi:[0,1] neg_lo:[0,1]
	v_pk_fma_f32 v[14:15], v[178:179], v[16:17], v[18:19] op_sel_hi:[1,0,1]
	s_nop 0
	v_pk_mul_f32 v[16:17], v[34:35], v[14:15] op_sel:[1,1] op_sel_hi:[1,0] neg_lo:[1,0]
	v_add_u32_e32 v10, 0x1ff80, v10
	v_pk_fma_f32 v[14:15], v[34:35], v[14:15], v[16:17] op_sel_hi:[0,1,1]
	ds_write_b64 v10, v[14:15]
	v_mov_b32_e32 v10, v174
	v_mov_b32_e32 v13, v172
	s_waitcnt lgkmcnt(0)
	s_barrier
	v_mov_b32_e32 v14, v180
	v_xad_u32 v28, v13, 3, v10
	v_lshl_add_u32 v71, v28, 3, 0
	v_xad_u32 v28, v13, 4, v10
	v_lshl_add_u32 v70, v28, 3, 0
	v_xad_u32 v28, v13, 5, v10
	v_lshl_add_u32 v69, v28, 3, 0
	v_xad_u32 v28, v13, 6, v10
	v_lshl_add_u32 v68, v28, 3, 0
	v_xad_u32 v28, v13, 7, v10
	v_lshl_add_u32 v67, v28, 3, 0
	v_xad_u32 v28, v13, 8, v10
	v_lshl_add_u32 v28, v28, 3, 0
	v_add_u32_e32 v66, 0x800, v28
	v_xad_u32 v28, v13, 9, v10
	v_lshl_add_u32 v28, v28, 3, 0
	v_add_u32_e32 v65, 0x800, v28
	v_xad_u32 v28, v13, 10, v10
	v_lshl_add_u32 v28, v28, 3, 0
	v_add_u32_e32 v64, 0x800, v28
	v_xad_u32 v28, v13, 11, v10
	v_lshl_add_u32 v28, v28, 3, 0
	v_add_u32_e32 v16, v13, v10
	v_add_u32_e32 v63, 0x800, v28
	v_xad_u32 v28, v13, 12, v10
	v_mov_b32_e32 v15, v181
	v_lshl_add_u32 v74, v16, 3, 0
	v_lshl_add_u32 v28, v28, 3, 0
	ds_read2_b64 v[16:19], v74 offset1:16
	ds_read2_b64 v[38:41], v66 offset1:16
	v_add_u32_e32 v62, 0x800, v28
	v_xad_u32 v28, v13, 13, v10
	v_xad_u32 v20, v13, 1, v10
	v_lshl_add_u32 v28, v28, 3, 0
	v_lshl_add_u32 v73, v20, 3, 0
	v_xad_u32 v24, v13, 2, v10
	v_add_u32_e32 v61, 0x800, v28
	v_xad_u32 v28, v13, 14, v10
	v_xad_u32 v10, v13, 15, v10
	ds_read2_b64 v[20:23], v73 offset0:32 offset1:48
	ds_read2_b64 v[46:49], v65 offset0:32 offset1:48
	v_lshl_add_u32 v28, v28, 3, 0
	v_lshl_add_u32 v10, v10, 3, 0
	v_lshl_add_u32 v72, v24, 3, 0
	v_add_u32_e32 v60, 0x800, v28
	v_add_u32_e32 v13, 0x800, v10
	ds_read2_b64 v[24:27], v72 offset0:64 offset1:80
	ds_read2_b64 v[56:59], v71 offset0:96 offset1:112
	ds_read2_b64 v[76:79], v70 offset0:128 offset1:144
	ds_read2_b64 v[80:83], v69 offset0:160 offset1:176
	ds_read2_b64 v[84:87], v68 offset0:192 offset1:208
	ds_read2_b64 v[88:91], v67 offset0:224 offset1:240
	ds_read2_b64 v[52:55], v64 offset0:64 offset1:80
	ds_read2_b64 v[92:95], v63 offset0:96 offset1:112
	ds_read2_b64 v[96:99], v62 offset0:128 offset1:144
	ds_read2_b64 v[100:103], v61 offset0:160 offset1:176
	ds_read2_b64 v[104:107], v60 offset0:192 offset1:208
	ds_read2_b64 v[108:111], v13 offset0:224 offset1:240
	s_waitcnt lgkmcnt(14)
	v_pk_add_f32 v[112:113], v[16:17], v[38:39]
	v_pk_add_f32 v[38:39], v[16:17], v[38:39] neg_lo:[0,1] neg_hi:[0,1]
	v_pk_add_f32 v[16:17], v[18:19], v[40:41]
	v_pk_add_f32 v[18:19], v[18:19], v[40:41] neg_lo:[0,1] neg_hi:[0,1]
	v_mov_b32_e32 v28, v164
	v_mov_b32_e32 v30, v165
	v_mov_b32_e32 v32, v166
	v_mov_b32_e32 v10, v167
	v_mov_b32_e32 v36, v168
	v_mov_b32_e32 v34, v169
	v_mov_b32_e32 v44, v170
	v_mov_b32_e32 v29, v171
	v_pk_mul_f32 v[40:41], v[18:19], v[44:45] op_sel:[1,0] op_sel_hi:[0,0] neg_lo:[1,1] neg_hi:[0,1]
	s_nop 0
	v_pk_fma_f32 v[42:43], v[18:19], v[28:29], v[40:41] op_sel_hi:[1,0,1]
	s_waitcnt lgkmcnt(12)
	v_pk_add_f32 v[18:19], v[20:21], v[46:47]
	v_pk_add_f32 v[20:21], v[20:21], v[46:47] neg_lo:[0,1] neg_hi:[0,1]
	s_nop 0
	v_pk_mul_f32 v[40:41], v[20:21], v[34:35] op_sel:[1,0] op_sel_hi:[0,0] neg_lo:[1,1] neg_hi:[0,1]
	s_nop 0
	v_pk_fma_f32 v[46:47], v[20:21], v[30:31], v[40:41] op_sel_hi:[1,0,1]
	v_pk_add_f32 v[20:21], v[22:23], v[48:49]
	v_pk_add_f32 v[22:23], v[22:23], v[48:49] neg_lo:[0,1] neg_hi:[0,1]
	s_nop 0
	v_pk_mul_f32 v[40:41], v[22:23], v[36:37] op_sel:[1,0] op_sel_hi:[0,0] neg_lo:[1,1] neg_hi:[0,1]
	s_nop 0
	v_pk_fma_f32 v[50:51], v[22:23], v[32:33], v[40:41] op_sel_hi:[1,0,1]
	s_waitcnt lgkmcnt(5)
	v_pk_add_f32 v[22:23], v[24:25], v[52:53]
	v_pk_add_f32 v[24:25], v[24:25], v[52:53] neg_lo:[0,1] neg_hi:[0,1]
	s_nop 0
	v_pk_mul_f32 v[40:41], v[24:25], v[10:11] op_sel:[1,0] op_sel_hi:[0,0] neg_lo:[1,1] neg_hi:[0,1]
	s_nop 0
	v_pk_fma_f32 v[52:53], v[24:25], v[10:11], v[40:41] op_sel_hi:[1,0,1]
	v_pk_add_f32 v[24:25], v[26:27], v[54:55]
	v_pk_add_f32 v[26:27], v[26:27], v[54:55] neg_lo:[0,1] neg_hi:[0,1]
	s_nop 0
	v_pk_mul_f32 v[40:41], v[26:27], v[36:37] op_sel_hi:[1,0]
	s_nop 0
	v_pk_fma_f32 v[54:55], v[26:27], v[32:33], v[40:41] op_sel:[1,0,0] op_sel_hi:[0,0,1] neg_lo:[1,1,0] neg_hi:[0,1,0]
	s_waitcnt lgkmcnt(4)
	v_pk_add_f32 v[40:41], v[56:57], v[92:93] neg_lo:[0,1] neg_hi:[0,1]
	v_pk_add_f32 v[26:27], v[56:57], v[92:93]
	v_pk_mul_f32 v[48:49], v[40:41], v[34:35] op_sel_hi:[1,0]
	s_nop 0
	v_pk_fma_f32 v[56:57], v[40:41], v[30:31], v[48:49] op_sel:[1,0,0] op_sel_hi:[0,0,1] neg_lo:[1,1,0] neg_hi:[0,1,0]
	v_pk_add_f32 v[48:49], v[58:59], v[94:95] neg_lo:[0,1] neg_hi:[0,1]
	v_pk_add_f32 v[40:41], v[58:59], v[94:95]
	v_pk_mul_f32 v[58:59], v[48:49], v[44:45] op_sel_hi:[1,0]
	v_xor_b32_e32 v92, 0x80000000, v49
	v_mov_b32_e32 v93, v48
	s_waitcnt lgkmcnt(3)
	v_pk_add_f32 v[48:49], v[76:77], v[96:97]
	v_pk_add_f32 v[76:77], v[76:77], v[96:97] neg_lo:[0,1] neg_hi:[0,1]
	v_pk_fma_f32 v[58:59], v[92:93], v[28:29], v[58:59] op_sel_hi:[1,0,1] neg_lo:[0,1,0] neg_hi:[0,1,0]
	v_xor_b32_e32 v93, 0x80000000, v76
	v_mov_b32_e32 v92, v77
	v_pk_add_f32 v[76:77], v[78:79], v[98:99]
	v_pk_add_f32 v[78:79], v[78:79], v[98:99] neg_lo:[0,1] neg_hi:[0,1]
	s_nop 0
	v_pk_mul_f32 v[94:95], v[78:79], v[44:45] op_sel_hi:[1,0] neg_lo:[0,1] neg_hi:[0,1]
	s_nop 0
	v_pk_fma_f32 v[78:79], v[78:79], v[28:29], v[94:95] op_sel:[1,0,0] op_sel_hi:[0,0,1] neg_lo:[1,1,0] neg_hi:[0,1,0]
	s_waitcnt lgkmcnt(2)
	v_pk_add_f32 v[94:95], v[80:81], v[100:101]
	v_pk_add_f32 v[80:81], v[80:81], v[100:101] neg_lo:[0,1] neg_hi:[0,1]
	s_nop 0
	v_pk_mul_f32 v[96:97], v[80:81], v[34:35] op_sel_hi:[1,0] neg_lo:[0,1] neg_hi:[0,1]
	s_nop 0
	v_pk_fma_f32 v[80:81], v[80:81], v[30:31], v[96:97] op_sel:[1,0,0] op_sel_hi:[0,0,1] neg_lo:[1,1,0] neg_hi:[0,1,0]
	v_pk_add_f32 v[96:97], v[82:83], v[102:103]
	v_pk_add_f32 v[82:83], v[82:83], v[102:103] neg_lo:[0,1] neg_hi:[0,1]
	s_nop 0
	v_pk_mul_f32 v[98:99], v[82:83], v[36:37] op_sel_hi:[1,0] neg_lo:[0,1] neg_hi:[0,1]
	s_nop 0
	v_pk_fma_f32 v[82:83], v[82:83], v[32:33], v[98:99] op_sel:[1,0,0] op_sel_hi:[0,0,1] neg_lo:[1,1,0] neg_hi:[0,1,0]
	s_waitcnt lgkmcnt(1)
	v_pk_add_f32 v[98:99], v[84:85], v[104:105]
	v_pk_add_f32 v[84:85], v[84:85], v[104:105] neg_lo:[0,1] neg_hi:[0,1]
	s_nop 0
	v_pk_mul_f32 v[100:101], v[84:85], v[10:11] op_sel:[1,0] op_sel_hi:[0,0] neg_lo:[1,1] neg_hi:[0,1]
	s_nop 0
	v_pk_fma_f32 v[84:85], v[84:85], v[10:11], v[100:101] op_sel_hi:[1,0,1] neg_lo:[0,1,0] neg_hi:[0,1,0]
	v_pk_add_f32 v[100:101], v[86:87], v[106:107]
	v_pk_add_f32 v[86:87], v[86:87], v[106:107] neg_lo:[0,1] neg_hi:[0,1]
	s_nop 0
	v_pk_mul_f32 v[36:37], v[86:87], v[36:37] op_sel:[1,0] op_sel_hi:[0,0] neg_lo:[1,1] neg_hi:[0,1]
	s_nop 0
	v_pk_fma_f32 v[86:87], v[86:87], v[32:33], v[36:37] op_sel_hi:[1,0,1] neg_lo:[0,1,0] neg_hi:[0,1,0]
	s_waitcnt lgkmcnt(0)
	v_pk_add_f32 v[36:37], v[88:89], v[108:109] neg_lo:[0,1] neg_hi:[0,1]
	v_pk_add_f32 v[32:33], v[88:89], v[108:109]
	v_pk_mul_f32 v[88:89], v[36:37], v[34:35] op_sel:[1,0] op_sel_hi:[0,0] neg_lo:[1,1] neg_hi:[0,1]
	s_nop 0
	v_pk_fma_f32 v[88:89], v[36:37], v[30:31], v[88:89] op_sel_hi:[1,0,1] neg_lo:[0,1,0] neg_hi:[0,1,0]
	v_pk_add_f32 v[36:37], v[90:91], v[110:111]
	v_pk_add_f32 v[90:91], v[90:91], v[110:111] neg_lo:[0,1] neg_hi:[0,1]
	s_nop 0
	v_pk_mul_f32 v[44:45], v[90:91], v[44:45] op_sel:[1,0] op_sel_hi:[0,0] neg_lo:[1,1] neg_hi:[0,1]
	s_nop 0
	v_pk_fma_f32 v[90:91], v[90:91], v[28:29], v[44:45] op_sel_hi:[1,0,1] neg_lo:[0,1,0] neg_hi:[0,1,0]
	v_pk_add_f32 v[44:45], v[16:17], v[76:77]
	v_pk_add_f32 v[16:17], v[16:17], v[76:77] neg_lo:[0,1] neg_hi:[0,1]
	v_pk_add_f32 v[28:29], v[112:113], v[48:49]
	v_pk_mul_f32 v[76:77], v[16:17], v[34:35] op_sel:[1,0] op_sel_hi:[0,0] neg_lo:[1,1] neg_hi:[0,1]
	v_pk_add_f32 v[48:49], v[112:113], v[48:49] neg_lo:[0,1] neg_hi:[0,1]
	v_pk_fma_f32 v[76:77], v[16:17], v[30:31], v[76:77] op_sel_hi:[1,0,1]
	v_pk_add_f32 v[16:17], v[18:19], v[94:95]
	v_pk_add_f32 v[18:19], v[18:19], v[94:95] neg_lo:[0,1] neg_hi:[0,1]
	s_nop 0
	v_pk_mul_f32 v[94:95], v[18:19], v[10:11] op_sel:[1,0] op_sel_hi:[0,0] neg_lo:[1,1] neg_hi:[0,1]
	s_nop 0
	v_pk_fma_f32 v[18:19], v[18:19], v[10:11], v[94:95] op_sel_hi:[1,0,1]
	v_pk_add_f32 v[94:95], v[20:21], v[96:97]
	v_pk_add_f32 v[20:21], v[20:21], v[96:97] neg_lo:[0,1] neg_hi:[0,1]
	s_nop 0
	v_pk_mul_f32 v[96:97], v[20:21], v[34:35] op_sel_hi:[1,0]
	v_xor_b32_e32 v102, 0x80000000, v21
	v_mov_b32_e32 v103, v20
	v_pk_add_f32 v[20:21], v[22:23], v[98:99]
	v_pk_add_f32 v[22:23], v[22:23], v[98:99] neg_lo:[0,1] neg_hi:[0,1]
	v_pk_fma_f32 v[96:97], v[102:103], v[30:31], v[96:97] op_sel_hi:[1,0,1] neg_lo:[0,1,0] neg_hi:[0,1,0]
	v_xor_b32_e32 v99, 0x80000000, v22
	v_mov_b32_e32 v98, v23
	v_pk_add_f32 v[22:23], v[24:25], v[100:101]
	v_pk_add_f32 v[24:25], v[24:25], v[100:101] neg_lo:[0,1] neg_hi:[0,1]
	s_nop 0
	v_pk_mul_f32 v[100:101], v[24:25], v[34:35] op_sel_hi:[1,0] neg_lo:[0,1] neg_hi:[0,1]
	v_xor_b32_e32 v102, 0x80000000, v25
	v_mov_b32_e32 v103, v24
	v_pk_add_f32 v[24:25], v[26:27], v[32:33]
	v_pk_add_f32 v[26:27], v[26:27], v[32:33] neg_lo:[0,1] neg_hi:[0,1]
	v_pk_fma_f32 v[100:101], v[102:103], v[30:31], v[100:101] op_sel_hi:[1,0,1] neg_lo:[0,1,0] neg_hi:[0,1,0]
	v_pk_mul_f32 v[32:33], v[26:27], v[10:11] op_sel:[1,0] op_sel_hi:[0,0] neg_lo:[1,1] neg_hi:[0,1]
	v_pk_add_f32 v[102:103], v[28:29], v[20:21] neg_lo:[0,1] neg_hi:[0,1]
	v_pk_fma_f32 v[26:27], v[26:27], v[10:11], v[32:33] op_sel_hi:[1,0,1] neg_lo:[0,1,0] neg_hi:[0,1,0]
	v_pk_add_f32 v[32:33], v[40:41], v[36:37]
	v_pk_add_f32 v[36:37], v[40:41], v[36:37] neg_lo:[0,1] neg_hi:[0,1]
	s_nop 0
	v_pk_mul_f32 v[40:41], v[36:37], v[34:35] op_sel:[1,0] op_sel_hi:[0,0] neg_lo:[1,1] neg_hi:[0,1]
	s_nop 0
	v_pk_fma_f32 v[40:41], v[36:37], v[30:31], v[40:41] op_sel_hi:[1,0,1] neg_lo:[0,1,0] neg_hi:[0,1,0]
	v_pk_add_f32 v[36:37], v[28:29], v[20:21]
	v_pk_add_f32 v[20:21], v[44:45], v[22:23]
	v_pk_add_f32 v[22:23], v[44:45], v[22:23] neg_lo:[0,1] neg_hi:[0,1]
	s_nop 0
	v_pk_mul_f32 v[28:29], v[22:23], v[10:11] op_sel:[1,0] op_sel_hi:[0,0] neg_lo:[1,1] neg_hi:[0,1]
	s_nop 0
	v_pk_fma_f32 v[22:23], v[22:23], v[10:11], v[28:29] op_sel_hi:[1,0,1]
	v_pk_add_f32 v[28:29], v[16:17], v[24:25]
	v_pk_add_f32 v[16:17], v[16:17], v[24:25] neg_lo:[0,1] neg_hi:[0,1]
	s_nop 0
	v_xor_b32_e32 v25, 0x80000000, v16
	v_mov_b32_e32 v24, v17
	v_pk_add_f32 v[16:17], v[94:95], v[32:33]
	v_pk_add_f32 v[32:33], v[94:95], v[32:33] neg_lo:[0,1] neg_hi:[0,1]
	s_nop 0
	v_pk_mul_f32 v[44:45], v[32:33], v[10:11] op_sel:[1,0] op_sel_hi:[0,0] neg_lo:[1,1] neg_hi:[0,1]
	s_nop 0
	v_pk_fma_f32 v[32:33], v[32:33], v[10:11], v[44:45] op_sel_hi:[1,0,1] neg_lo:[0,1,0] neg_hi:[0,1,0]
	v_pk_add_f32 v[44:45], v[36:37], v[28:29]
	v_pk_add_f32 v[36:37], v[36:37], v[28:29] neg_lo:[0,1] neg_hi:[0,1]
	v_pk_add_f32 v[28:29], v[20:21], v[16:17]
	v_pk_add_f32 v[16:17], v[20:21], v[16:17] neg_lo:[0,1] neg_hi:[0,1]
	v_pk_add_f32 v[94:95], v[44:45], v[28:29]
	v_xor_b32_e32 v21, 0x80000000, v16
	v_mov_b32_e32 v20, v17
	v_pk_add_f32 v[16:17], v[102:103], v[24:25]
	v_pk_add_f32 v[102:103], v[102:103], v[24:25] neg_lo:[0,1] neg_hi:[0,1]
	v_pk_add_f32 v[24:25], v[22:23], v[32:33]
	v_pk_add_f32 v[22:23], v[22:23], v[32:33] neg_lo:[0,1] neg_hi:[0,1]
	v_pk_add_f32 v[28:29], v[44:45], v[28:29] neg_lo:[0,1] neg_hi:[0,1]
	v_xor_b32_e32 v33, 0x80000000, v22
	v_mov_b32_e32 v32, v23
	v_pk_add_f32 v[22:23], v[48:49], v[98:99]
	v_pk_add_f32 v[98:99], v[48:49], v[98:99] neg_lo:[0,1] neg_hi:[0,1]
	v_pk_add_f32 v[48:49], v[76:77], v[100:101] neg_lo:[0,1] neg_hi:[0,1]
	v_pk_add_f32 v[44:45], v[36:37], v[20:21]
	v_pk_add_f32 v[20:21], v[36:37], v[20:21] neg_lo:[0,1] neg_hi:[0,1]
	v_pk_add_f32 v[104:105], v[16:17], v[24:25]
	v_pk_add_f32 v[24:25], v[16:17], v[24:25] neg_lo:[0,1] neg_hi:[0,1]
	v_pk_add_f32 v[36:37], v[102:103], v[32:33]
	v_pk_add_f32 v[16:17], v[102:103], v[32:33] neg_lo:[0,1] neg_hi:[0,1]
	v_pk_add_f32 v[32:33], v[76:77], v[100:101]
	v_pk_mul_f32 v[76:77], v[10:11], v[48:49] op_sel:[0,1] op_sel_hi:[0,0] neg_lo:[1,1] neg_hi:[1,0]
	v_pk_fma_f32 v[76:77], v[10:11], v[48:49], v[76:77] op_sel_hi:[0,1,1]
	v_pk_add_f32 v[48:49], v[18:19], v[26:27]
	v_pk_add_f32 v[18:19], v[18:19], v[26:27] neg_lo:[0,1] neg_hi:[0,1]
	s_nop 0
	v_xor_b32_e32 v27, 0x80000000, v18
	v_mov_b32_e32 v26, v19
	v_pk_add_f32 v[18:19], v[96:97], v[40:41]
	v_pk_add_f32 v[40:41], v[96:97], v[40:41] neg_lo:[0,1] neg_hi:[0,1]
	s_nop 0
	v_pk_mul_f32 v[96:97], v[10:11], v[40:41] op_sel:[0,1] op_sel_hi:[0,0] neg_lo:[1,1] neg_hi:[1,0]
	v_pk_fma_f32 v[40:41], v[10:11], v[40:41], v[96:97] op_sel_hi:[0,1,1] neg_lo:[1,0,0] neg_hi:[1,0,0]
	v_pk_add_f32 v[96:97], v[22:23], v[48:49]
	v_pk_add_f32 v[22:23], v[22:23], v[48:49] neg_lo:[0,1] neg_hi:[0,1]
	v_pk_add_f32 v[48:49], v[32:33], v[18:19]
	v_pk_add_f32 v[18:19], v[32:33], v[18:19] neg_lo:[0,1] neg_hi:[0,1]
	v_pk_add_f32 v[102:103], v[96:97], v[48:49]
	v_xor_b32_e32 v101, 0x80000000, v18
	v_mov_b32_e32 v100, v19
	v_pk_add_f32 v[32:33], v[96:97], v[48:49] neg_lo:[0,1] neg_hi:[0,1]
	v_pk_add_f32 v[18:19], v[98:99], v[26:27]
	v_pk_add_f32 v[96:97], v[98:99], v[26:27] neg_lo:[0,1] neg_hi:[0,1]
	v_pk_add_f32 v[26:27], v[76:77], v[40:41]
	v_pk_add_f32 v[40:41], v[76:77], v[40:41] neg_lo:[0,1] neg_hi:[0,1]
	v_pk_add_f32 v[98:99], v[18:19], v[26:27]
	v_xor_b32_e32 v77, 0x80000000, v40
	v_mov_b32_e32 v76, v41
	v_pk_add_f32 v[26:27], v[18:19], v[26:27] neg_lo:[0,1] neg_hi:[0,1]
	v_pk_add_f32 v[40:41], v[96:97], v[76:77]
	v_pk_add_f32 v[18:19], v[96:97], v[76:77] neg_lo:[0,1] neg_hi:[0,1]
	v_pk_add_f32 v[76:77], v[38:39], v[92:93]
	v_pk_add_f32 v[92:93], v[38:39], v[92:93] neg_lo:[0,1] neg_hi:[0,1]
	v_pk_add_f32 v[38:39], v[42:43], v[78:79]
	v_pk_add_f32 v[42:43], v[42:43], v[78:79] neg_lo:[0,1] neg_hi:[0,1]
	v_pk_add_f32 v[48:49], v[22:23], v[100:101]
	v_pk_mul_f32 v[78:79], v[34:35], v[42:43] op_sel:[0,1] op_sel_hi:[0,0] neg_lo:[1,1] neg_hi:[1,0]
	v_pk_fma_f32 v[42:43], v[30:31], v[42:43], v[78:79] op_sel_hi:[0,1,1]
	v_pk_add_f32 v[78:79], v[46:47], v[80:81]
	v_pk_add_f32 v[46:47], v[46:47], v[80:81] neg_lo:[0,1] neg_hi:[0,1]
	v_pk_add_f32 v[22:23], v[22:23], v[100:101] neg_lo:[0,1] neg_hi:[0,1]
	v_pk_mul_f32 v[80:81], v[10:11], v[46:47] op_sel:[0,1] op_sel_hi:[0,0] neg_lo:[1,1] neg_hi:[1,0]
	v_pk_fma_f32 v[80:81], v[10:11], v[46:47], v[80:81] op_sel_hi:[0,1,1]
	v_pk_add_f32 v[46:47], v[50:51], v[82:83]
	v_pk_add_f32 v[50:51], v[50:51], v[82:83] neg_lo:[0,1] neg_hi:[0,1]
	s_nop 0
	v_pk_mul_f32 v[82:83], v[30:31], v[50:51] op_sel:[0,1] op_sel_hi:[0,0] neg_lo:[1,1] neg_hi:[1,0]
	v_pk_fma_f32 v[50:51], v[34:35], v[50:51], v[82:83] op_sel_hi:[0,1,1]
	v_pk_add_f32 v[82:83], v[52:53], v[84:85]
	v_pk_add_f32 v[52:53], v[52:53], v[84:85] neg_lo:[0,1] neg_hi:[0,1]
	s_nop 0
	v_xor_b32_e32 v85, 0x80000000, v52
	v_mov_b32_e32 v84, v53
	v_pk_add_f32 v[52:53], v[54:55], v[86:87]
	v_pk_add_f32 v[54:55], v[54:55], v[86:87] neg_lo:[0,1] neg_hi:[0,1]
	s_nop 0
	v_pk_mul_f32 v[86:87], v[30:31], v[54:55] op_sel:[0,1] op_sel_hi:[0,0] neg_lo:[1,1] neg_hi:[1,0]
	v_pk_fma_f32 v[54:55], v[34:35], v[54:55], v[86:87] op_sel_hi:[0,1,1] neg_lo:[1,0,0] neg_hi:[1,0,0]
	v_pk_add_f32 v[86:87], v[56:57], v[88:89]
	v_pk_add_f32 v[56:57], v[56:57], v[88:89] neg_lo:[0,1] neg_hi:[0,1]
	s_nop 0
	v_pk_mul_f32 v[88:89], v[10:11], v[56:57] op_sel:[0,1] op_sel_hi:[0,0] neg_lo:[1,1] neg_hi:[1,0]
	v_pk_fma_f32 v[56:57], v[10:11], v[56:57], v[88:89] op_sel_hi:[0,1,1] neg_lo:[1,0,0] neg_hi:[1,0,0]
	v_pk_add_f32 v[88:89], v[58:59], v[90:91]
	v_pk_add_f32 v[58:59], v[58:59], v[90:91] neg_lo:[0,1] neg_hi:[0,1]
	s_nop 0
	v_pk_mul_f32 v[34:35], v[34:35], v[58:59] op_sel:[0,1] op_sel_hi:[0,0] neg_lo:[1,1] neg_hi:[1,0]
	v_pk_fma_f32 v[34:35], v[30:31], v[58:59], v[34:35] op_sel_hi:[0,1,1] neg_lo:[1,0,0] neg_hi:[1,0,0]
	v_pk_add_f32 v[30:31], v[76:77], v[82:83]
	v_pk_add_f32 v[58:59], v[76:77], v[82:83] neg_lo:[0,1] neg_hi:[0,1]
	v_pk_add_f32 v[76:77], v[52:53], v[38:39]
	v_pk_add_f32 v[38:39], v[38:39], v[52:53] neg_lo:[0,1] neg_hi:[0,1]
	s_nop 0
	v_pk_mul_f32 v[52:53], v[10:11], v[38:39] op_sel:[0,1] op_sel_hi:[0,0] neg_lo:[1,1] neg_hi:[1,0]
	v_pk_fma_f32 v[52:53], v[10:11], v[38:39], v[52:53] op_sel_hi:[0,1,1]
	v_pk_add_f32 v[38:39], v[78:79], v[86:87]
	v_pk_add_f32 v[78:79], v[78:79], v[86:87] neg_lo:[0,1] neg_hi:[0,1]
	s_nop 0
	v_xor_b32_e32 v83, 0x80000000, v78
	v_mov_b32_e32 v82, v79
	v_pk_add_f32 v[78:79], v[46:47], v[88:89]
	v_pk_add_f32 v[46:47], v[46:47], v[88:89] neg_lo:[0,1] neg_hi:[0,1]
	v_pk_add_f32 v[88:89], v[76:77], v[78:79]
	v_pk_mul_f32 v[86:87], v[10:11], v[46:47] op_sel:[0,1] op_sel_hi:[0,0] neg_lo:[1,1] neg_hi:[1,0]
	v_pk_fma_f32 v[46:47], v[10:11], v[46:47], v[86:87] op_sel_hi:[0,1,1] neg_lo:[1,0,0] neg_hi:[1,0,0]
	v_pk_add_f32 v[86:87], v[30:31], v[38:39]
	v_pk_add_f32 v[30:31], v[30:31], v[38:39] neg_lo:[0,1] neg_hi:[0,1]
	v_pk_add_f32 v[38:39], v[76:77], v[78:79] neg_lo:[0,1] neg_hi:[0,1]
	v_pk_add_f32 v[78:79], v[86:87], v[88:89] neg_lo:[0,1] neg_hi:[0,1]
	v_pk_add_f32 v[90:91], v[30:31], v[38:39] op_sel:[0,1] op_sel_hi:[1,0] neg_hi:[0,1]
	v_pk_add_f32 v[38:39], v[30:31], v[38:39] op_sel:[0,1] op_sel_hi:[1,0] neg_lo:[0,1]
	v_pk_add_f32 v[76:77], v[52:53], v[46:47]
	v_pk_add_f32 v[46:47], v[52:53], v[46:47] neg_lo:[0,1] neg_hi:[0,1]
	v_pk_add_f32 v[30:31], v[58:59], v[82:83]
	v_pk_add_f32 v[58:59], v[58:59], v[82:83] neg_lo:[0,1] neg_hi:[0,1]
	v_xor_b32_e32 v53, 0x80000000, v46
	v_mov_b32_e32 v52, v47
	v_pk_add_f32 v[82:83], v[30:31], v[76:77]
	v_pk_add_f32 v[46:47], v[30:31], v[76:77] neg_lo:[0,1] neg_hi:[0,1]
	v_pk_add_f32 v[76:77], v[58:59], v[52:53]
	v_pk_add_f32 v[30:31], v[58:59], v[52:53] neg_lo:[0,1] neg_hi:[0,1]
	v_pk_add_f32 v[52:53], v[92:93], v[84:85]
	v_pk_add_f32 v[58:59], v[92:93], v[84:85] neg_lo:[0,1] neg_hi:[0,1]
	v_pk_add_f32 v[84:85], v[54:55], v[42:43]
	v_pk_add_f32 v[42:43], v[42:43], v[54:55] neg_lo:[0,1] neg_hi:[0,1]
	v_pk_add_f32 v[86:87], v[86:87], v[88:89]
	v_pk_mul_f32 v[54:55], v[10:11], v[42:43] op_sel:[0,1] op_sel_hi:[0,0] neg_lo:[1,1] neg_hi:[1,0]
	v_pk_fma_f32 v[54:55], v[10:11], v[42:43], v[54:55] op_sel_hi:[0,1,1]
	v_pk_add_f32 v[42:43], v[80:81], v[56:57]
	v_pk_add_f32 v[56:57], v[80:81], v[56:57] neg_lo:[0,1] neg_hi:[0,1]
	s_nop 0
	v_xor_b32_e32 v81, 0x80000000, v56
	v_mov_b32_e32 v80, v57
	v_pk_add_f32 v[56:57], v[50:51], v[34:35]
	v_pk_add_f32 v[34:35], v[50:51], v[34:35] neg_lo:[0,1] neg_hi:[0,1]
	s_nop 0
	v_pk_mul_f32 v[50:51], v[10:11], v[34:35] op_sel:[0,1] op_sel_hi:[0,0] neg_lo:[1,1] neg_hi:[1,0]
	v_pk_fma_f32 v[34:35], v[10:11], v[34:35], v[50:51] op_sel_hi:[0,1,1] neg_lo:[1,0,0] neg_hi:[1,0,0]
	v_pk_add_f32 v[50:51], v[52:53], v[42:43]
	v_pk_add_f32 v[42:43], v[52:53], v[42:43] neg_lo:[0,1] neg_hi:[0,1]
	v_pk_add_f32 v[52:53], v[84:85], v[56:57]
	v_pk_add_f32 v[56:57], v[84:85], v[56:57] neg_lo:[0,1] neg_hi:[0,1]
	s_nop 0
	v_xor_b32_e32 v85, 0x80000000, v56
	v_mov_b32_e32 v84, v57
	v_pk_add_f32 v[56:57], v[50:51], v[52:53]
	v_pk_add_f32 v[50:51], v[50:51], v[52:53] neg_lo:[0,1] neg_hi:[0,1]
	v_pk_add_f32 v[52:53], v[42:43], v[84:85]
	v_pk_add_f32 v[42:43], v[42:43], v[84:85] neg_lo:[0,1] neg_hi:[0,1]
	v_pk_add_f32 v[84:85], v[58:59], v[80:81]
	v_pk_add_f32 v[58:59], v[58:59], v[80:81] neg_lo:[0,1] neg_hi:[0,1]
	v_pk_add_f32 v[80:81], v[54:55], v[34:35]
	v_pk_add_f32 v[34:35], v[54:55], v[34:35] neg_lo:[0,1] neg_hi:[0,1]
	v_pk_add_f32 v[92:93], v[84:85], v[80:81]
	v_pk_add_f32 v[80:81], v[84:85], v[80:81] neg_lo:[0,1] neg_hi:[0,1]
	v_pk_add_f32 v[84:85], v[58:59], v[34:35] op_sel:[0,1] op_sel_hi:[1,0] neg_hi:[0,1]
	v_pk_add_f32 v[34:35], v[58:59], v[34:35] op_sel:[0,1] op_sel_hi:[1,0] neg_lo:[0,1]
	v_pk_fma_f32 v[58:59], v[14:15], s[90:91], v[14:15] op_sel:[1,0,0] op_sel_hi:[0,1,1]
	v_pk_mul_f32 v[54:55], v[94:95], s[14:15] op_sel:[1,0] neg_lo:[1,0]
	v_pk_mul_f32 v[88:89], v[58:59], v[86:87] op_sel:[1,1] op_sel_hi:[0,1] neg_lo:[0,1]
	v_pk_fma_f32 v[54:55], v[94:95], s[94:95], v[54:55] op_sel_hi:[0,1,1]
	v_pk_fma_f32 v[86:87], v[58:59], v[86:87], v[88:89] op_sel_hi:[1,0,1]
	ds_write2_b64 v74, v[54:55], v[86:87] offset1:16
	v_pk_mul_f32 v[54:55], v[14:15], v[58:59] op_sel:[1,1] op_sel_hi:[0,1] neg_lo:[0,1]
	v_pk_fma_f32 v[54:55], v[14:15], v[58:59], v[54:55] op_sel_hi:[1,0,1]
	s_nop 0
	v_pk_mul_f32 v[58:59], v[54:55], v[102:103] op_sel:[1,1] op_sel_hi:[0,1] neg_lo:[0,1]
	v_pk_mul_f32 v[74:75], v[14:15], v[54:55] op_sel:[1,1] op_sel_hi:[0,1] neg_lo:[0,1]
	v_pk_fma_f32 v[58:59], v[54:55], v[102:103], v[58:59] op_sel_hi:[1,0,1]
	v_pk_fma_f32 v[54:55], v[14:15], v[54:55], v[74:75] op_sel_hi:[1,0,1]
	s_nop 0
	v_pk_mul_f32 v[74:75], v[54:55], v[56:57] op_sel:[1,1] op_sel_hi:[0,1] neg_lo:[0,1]
	v_pk_fma_f32 v[56:57], v[54:55], v[56:57], v[74:75] op_sel_hi:[1,0,1]
	ds_write2_b64 v73, v[58:59], v[56:57] offset0:32 offset1:48
	v_pk_mul_f32 v[56:57], v[14:15], v[54:55] op_sel:[1,1] op_sel_hi:[0,1] neg_lo:[0,1]
	v_pk_fma_f32 v[54:55], v[14:15], v[54:55], v[56:57] op_sel_hi:[1,0,1]
	s_nop 0
	v_pk_mul_f32 v[56:57], v[54:55], v[104:105] op_sel:[1,1] op_sel_hi:[0,1] neg_lo:[0,1]
	v_pk_mul_f32 v[58:59], v[14:15], v[54:55] op_sel:[1,1] op_sel_hi:[0,1] neg_lo:[0,1]
	v_pk_fma_f32 v[56:57], v[54:55], v[104:105], v[56:57] op_sel_hi:[1,0,1]
	v_pk_fma_f32 v[54:55], v[14:15], v[54:55], v[58:59] op_sel_hi:[1,0,1]
	s_nop 0
	v_pk_mul_f32 v[58:59], v[54:55], v[82:83] op_sel:[1,1] op_sel_hi:[0,1] neg_lo:[0,1]
	v_pk_fma_f32 v[58:59], v[54:55], v[82:83], v[58:59] op_sel_hi:[1,0,1]
	ds_write2_b64 v72, v[56:57], v[58:59] offset0:64 offset1:80
	v_pk_mul_f32 v[56:57], v[14:15], v[54:55] op_sel:[1,1] op_sel_hi:[0,1] neg_lo:[0,1]
	v_pk_fma_f32 v[54:55], v[14:15], v[54:55], v[56:57] op_sel_hi:[1,0,1]
	s_nop 0
	v_pk_mul_f32 v[56:57], v[54:55], v[98:99] op_sel:[1,1] op_sel_hi:[0,1] neg_lo:[0,1]
	v_pk_mul_f32 v[58:59], v[14:15], v[54:55] op_sel:[1,1] op_sel_hi:[0,1] neg_lo:[0,1]
	v_pk_fma_f32 v[56:57], v[54:55], v[98:99], v[56:57] op_sel_hi:[1,0,1]
	v_pk_fma_f32 v[54:55], v[14:15], v[54:55], v[58:59] op_sel_hi:[1,0,1]
	s_nop 0
	v_pk_mul_f32 v[58:59], v[54:55], v[92:93] op_sel:[1,1] op_sel_hi:[0,1] neg_lo:[0,1]
	v_pk_fma_f32 v[58:59], v[54:55], v[92:93], v[58:59] op_sel_hi:[1,0,1]
	ds_write2_b64 v71, v[56:57], v[58:59] offset0:96 offset1:112
	v_pk_mul_f32 v[56:57], v[14:15], v[54:55] op_sel:[1,1] op_sel_hi:[0,1] neg_lo:[0,1]
	v_pk_fma_f32 v[54:55], v[14:15], v[54:55], v[56:57] op_sel_hi:[1,0,1]
	s_nop 0
	v_pk_mul_f32 v[56:57], v[54:55], v[44:45] op_sel:[1,1] op_sel_hi:[0,1] neg_lo:[0,1]
	v_pk_fma_f32 v[44:45], v[54:55], v[44:45], v[56:57] op_sel_hi:[1,0,1]
	v_pk_mul_f32 v[56:57], v[14:15], v[54:55] op_sel:[1,1] op_sel_hi:[0,1] neg_lo:[0,1]
	v_pk_fma_f32 v[54:55], v[14:15], v[54:55], v[56:57] op_sel_hi:[1,0,1]
	s_nop 0
	v_pk_mul_f32 v[56:57], v[54:55], v[90:91] op_sel:[1,1] op_sel_hi:[0,1] neg_lo:[0,1]
	v_pk_fma_f32 v[56:57], v[54:55], v[90:91], v[56:57] op_sel_hi:[1,0,1]
	ds_write2_b64 v70, v[44:45], v[56:57] offset0:128 offset1:144
	v_pk_mul_f32 v[44:45], v[14:15], v[54:55] op_sel:[1,1] op_sel_hi:[0,1] neg_lo:[0,1]
	v_pk_fma_f32 v[44:45], v[14:15], v[54:55], v[44:45] op_sel_hi:[1,0,1]
	s_nop 0
	v_pk_mul_f32 v[54:55], v[44:45], v[48:49] op_sel:[1,1] op_sel_hi:[0,1] neg_lo:[0,1]
	v_pk_fma_f32 v[48:49], v[44:45], v[48:49], v[54:55] op_sel_hi:[1,0,1]
	v_pk_mul_f32 v[54:55], v[14:15], v[44:45] op_sel:[1,1] op_sel_hi:[0,1] neg_lo:[0,1]
	v_pk_fma_f32 v[44:45], v[14:15], v[44:45], v[54:55] op_sel_hi:[1,0,1]
	s_nop 0
	v_pk_mul_f32 v[54:55], v[44:45], v[52:53] op_sel:[1,1] op_sel_hi:[0,1] neg_lo:[0,1]
	v_pk_fma_f32 v[52:53], v[44:45], v[52:53], v[54:55] op_sel_hi:[1,0,1]
	ds_write2_b64 v69, v[48:49], v[52:53] offset0:160 offset1:176
	v_pk_mul_f32 v[48:49], v[14:15], v[44:45] op_sel:[1,1] op_sel_hi:[0,1] neg_lo:[0,1]
	v_pk_fma_f32 v[44:45], v[14:15], v[44:45], v[48:49] op_sel_hi:[1,0,1]
	s_nop 0
	v_pk_mul_f32 v[48:49], v[36:37], v[44:45] op_sel:[1,1] op_sel_hi:[1,0] neg_lo:[1,0]
	s_nop 0
	v_pk_fma_f32 v[36:37], v[36:37], v[44:45], v[48:49] op_sel_hi:[0,1,1]
	v_pk_mul_f32 v[48:49], v[14:15], v[44:45] op_sel:[1,1] op_sel_hi:[0,1] neg_lo:[0,1]
	v_pk_fma_f32 v[44:45], v[14:15], v[44:45], v[48:49] op_sel_hi:[1,0,1]
	s_nop 0
	v_pk_mul_f32 v[48:49], v[44:45], v[76:77] op_sel:[1,1] op_sel_hi:[0,1] neg_lo:[0,1]
	v_pk_fma_f32 v[48:49], v[44:45], v[76:77], v[48:49] op_sel_hi:[1,0,1]
	ds_write2_b64 v68, v[36:37], v[48:49] offset0:192 offset1:208
	v_pk_mul_f32 v[36:37], v[14:15], v[44:45] op_sel:[1,1] op_sel_hi:[0,1] neg_lo:[0,1]
	v_pk_fma_f32 v[36:37], v[14:15], v[44:45], v[36:37] op_sel_hi:[1,0,1]
	s_nop 0
	v_pk_mul_f32 v[44:45], v[40:41], v[36:37] op_sel:[1,1] op_sel_hi:[1,0] neg_lo:[1,0]
	s_nop 0
	v_pk_fma_f32 v[40:41], v[40:41], v[36:37], v[44:45] op_sel_hi:[0,1,1]
	v_pk_mul_f32 v[44:45], v[14:15], v[36:37] op_sel:[1,1] op_sel_hi:[0,1] neg_lo:[0,1]
	v_pk_fma_f32 v[36:37], v[14:15], v[36:37], v[44:45] op_sel_hi:[1,0,1]
	s_nop 0
	v_pk_mul_f32 v[44:45], v[36:37], v[84:85] op_sel:[1,1] op_sel_hi:[0,1] neg_lo:[0,1]
	v_pk_fma_f32 v[44:45], v[36:37], v[84:85], v[44:45] op_sel_hi:[1,0,1]
	ds_write2_b64 v67, v[40:41], v[44:45] offset0:224 offset1:240
	v_pk_mul_f32 v[40:41], v[14:15], v[36:37] op_sel:[1,1] op_sel_hi:[0,1] neg_lo:[0,1]
	v_pk_fma_f32 v[36:37], v[14:15], v[36:37], v[40:41] op_sel_hi:[1,0,1]
	s_nop 0
	v_pk_mul_f32 v[40:41], v[28:29], v[36:37] op_sel:[1,1] op_sel_hi:[1,0] neg_lo:[1,0]
	s_nop 0
	v_pk_fma_f32 v[28:29], v[28:29], v[36:37], v[40:41] op_sel_hi:[0,1,1]
	v_pk_mul_f32 v[40:41], v[14:15], v[36:37] op_sel:[1,1] op_sel_hi:[0,1] neg_lo:[0,1]
	v_pk_fma_f32 v[36:37], v[14:15], v[36:37], v[40:41] op_sel_hi:[1,0,1]
	s_nop 0
	v_pk_mul_f32 v[40:41], v[78:79], v[36:37] op_sel:[1,1] op_sel_hi:[1,0] neg_lo:[1,0]
	s_nop 0
	v_pk_fma_f32 v[40:41], v[78:79], v[36:37], v[40:41] op_sel_hi:[0,1,1]
	ds_write2_b64 v66, v[28:29], v[40:41] offset1:16
	v_pk_mul_f32 v[28:29], v[14:15], v[36:37] op_sel:[1,1] op_sel_hi:[0,1] neg_lo:[0,1]
	v_pk_fma_f32 v[28:29], v[14:15], v[36:37], v[28:29] op_sel_hi:[1,0,1]
	s_nop 0
	v_pk_mul_f32 v[36:37], v[32:33], v[28:29] op_sel:[1,1] op_sel_hi:[1,0] neg_lo:[1,0]
	s_nop 0
	v_pk_fma_f32 v[32:33], v[32:33], v[28:29], v[36:37] op_sel_hi:[0,1,1]
	v_pk_mul_f32 v[36:37], v[14:15], v[28:29] op_sel:[1,1] op_sel_hi:[0,1] neg_lo:[0,1]
	v_pk_fma_f32 v[28:29], v[14:15], v[28:29], v[36:37] op_sel_hi:[1,0,1]
	s_nop 0
	v_pk_mul_f32 v[36:37], v[50:51], v[28:29] op_sel:[1,1] op_sel_hi:[1,0] neg_lo:[1,0]
	s_nop 0
	v_pk_fma_f32 v[36:37], v[50:51], v[28:29], v[36:37] op_sel_hi:[0,1,1]
	ds_write2_b64 v65, v[32:33], v[36:37] offset0:32 offset1:48
	v_pk_mul_f32 v[32:33], v[14:15], v[28:29] op_sel:[1,1] op_sel_hi:[0,1] neg_lo:[0,1]
	v_pk_fma_f32 v[28:29], v[14:15], v[28:29], v[32:33] op_sel_hi:[1,0,1]
	s_nop 0
	v_pk_mul_f32 v[32:33], v[24:25], v[28:29] op_sel:[1,1] op_sel_hi:[1,0] neg_lo:[1,0]
	s_nop 0
	v_pk_fma_f32 v[24:25], v[24:25], v[28:29], v[32:33] op_sel_hi:[0,1,1]
	v_pk_mul_f32 v[32:33], v[14:15], v[28:29] op_sel:[1,1] op_sel_hi:[0,1] neg_lo:[0,1]
	v_pk_fma_f32 v[28:29], v[14:15], v[28:29], v[32:33] op_sel_hi:[1,0,1]
	s_nop 0
	v_pk_mul_f32 v[32:33], v[46:47], v[28:29] op_sel:[1,1] op_sel_hi:[1,0] neg_lo:[1,0]
	s_nop 0
	v_pk_fma_f32 v[32:33], v[46:47], v[28:29], v[32:33] op_sel_hi:[0,1,1]
	ds_write2_b64 v64, v[24:25], v[32:33] offset0:64 offset1:80
	v_pk_mul_f32 v[24:25], v[14:15], v[28:29] op_sel:[1,1] op_sel_hi:[0,1] neg_lo:[0,1]
	v_pk_fma_f32 v[24:25], v[14:15], v[28:29], v[24:25] op_sel_hi:[1,0,1]
	s_nop 0
	v_pk_mul_f32 v[28:29], v[26:27], v[24:25] op_sel:[1,1] op_sel_hi:[1,0] neg_lo:[1,0]
	s_nop 0
	v_pk_fma_f32 v[26:27], v[26:27], v[24:25], v[28:29] op_sel_hi:[0,1,1]
	v_pk_mul_f32 v[28:29], v[14:15], v[24:25] op_sel:[1,1] op_sel_hi:[0,1] neg_lo:[0,1]
	v_pk_fma_f32 v[24:25], v[14:15], v[24:25], v[28:29] op_sel_hi:[1,0,1]
	s_nop 0
	v_pk_mul_f32 v[28:29], v[80:81], v[24:25] op_sel:[1,1] op_sel_hi:[1,0] neg_lo:[1,0]
	s_nop 0
	v_pk_fma_f32 v[28:29], v[80:81], v[24:25], v[28:29] op_sel_hi:[0,1,1]
	ds_write2_b64 v63, v[26:27], v[28:29] offset0:96 offset1:112
	v_pk_mul_f32 v[26:27], v[14:15], v[24:25] op_sel:[1,1] op_sel_hi:[0,1] neg_lo:[0,1]
	v_pk_fma_f32 v[24:25], v[14:15], v[24:25], v[26:27] op_sel_hi:[1,0,1]
	s_nop 0
	v_pk_mul_f32 v[26:27], v[20:21], v[24:25] op_sel:[1,1] op_sel_hi:[1,0] neg_lo:[1,0]
	s_nop 0
	v_pk_fma_f32 v[20:21], v[20:21], v[24:25], v[26:27] op_sel_hi:[0,1,1]
	v_pk_mul_f32 v[26:27], v[14:15], v[24:25] op_sel:[1,1] op_sel_hi:[0,1] neg_lo:[0,1]
	v_pk_fma_f32 v[24:25], v[14:15], v[24:25], v[26:27] op_sel_hi:[1,0,1]
	s_nop 0
	v_pk_mul_f32 v[26:27], v[38:39], v[24:25] op_sel:[1,1] op_sel_hi:[1,0] neg_lo:[1,0]
	s_nop 0
	v_pk_fma_f32 v[26:27], v[38:39], v[24:25], v[26:27] op_sel_hi:[0,1,1]
	ds_write2_b64 v62, v[20:21], v[26:27] offset0:128 offset1:144
	v_pk_mul_f32 v[20:21], v[14:15], v[24:25] op_sel:[1,1] op_sel_hi:[0,1] neg_lo:[0,1]
	v_pk_fma_f32 v[20:21], v[14:15], v[24:25], v[20:21] op_sel_hi:[1,0,1]
	s_nop 0
	v_pk_mul_f32 v[24:25], v[22:23], v[20:21] op_sel:[1,1] op_sel_hi:[1,0] neg_lo:[1,0]
	s_nop 0
	v_pk_fma_f32 v[22:23], v[22:23], v[20:21], v[24:25] op_sel_hi:[0,1,1]
	v_pk_mul_f32 v[24:25], v[14:15], v[20:21] op_sel:[1,1] op_sel_hi:[0,1] neg_lo:[0,1]
	v_pk_fma_f32 v[20:21], v[14:15], v[20:21], v[24:25] op_sel_hi:[1,0,1]
	s_nop 0
	v_pk_mul_f32 v[24:25], v[42:43], v[20:21] op_sel:[1,1] op_sel_hi:[1,0] neg_lo:[1,0]
	s_nop 0
	v_pk_fma_f32 v[24:25], v[42:43], v[20:21], v[24:25] op_sel_hi:[0,1,1]
	ds_write2_b64 v61, v[22:23], v[24:25] offset0:160 offset1:176
	v_pk_mul_f32 v[22:23], v[14:15], v[20:21] op_sel:[1,1] op_sel_hi:[0,1] neg_lo:[0,1]
	v_pk_fma_f32 v[20:21], v[14:15], v[20:21], v[22:23] op_sel_hi:[1,0,1]
	s_nop 0
	v_pk_mul_f32 v[22:23], v[16:17], v[20:21] op_sel:[1,1] op_sel_hi:[1,0] neg_lo:[1,0]
	s_nop 0
	v_pk_fma_f32 v[16:17], v[16:17], v[20:21], v[22:23] op_sel_hi:[0,1,1]
	v_pk_mul_f32 v[22:23], v[14:15], v[20:21] op_sel:[1,1] op_sel_hi:[0,1] neg_lo:[0,1]
	v_pk_fma_f32 v[20:21], v[14:15], v[20:21], v[22:23] op_sel_hi:[1,0,1]
	s_nop 0
	v_pk_mul_f32 v[22:23], v[30:31], v[20:21] op_sel:[1,1] op_sel_hi:[1,0] neg_lo:[1,0]
	s_nop 0
	v_pk_fma_f32 v[22:23], v[30:31], v[20:21], v[22:23] op_sel_hi:[0,1,1]
	ds_write2_b64 v60, v[16:17], v[22:23] offset0:192 offset1:208
	v_pk_mul_f32 v[16:17], v[14:15], v[20:21] op_sel:[1,1] op_sel_hi:[0,1] neg_lo:[0,1]
	v_pk_fma_f32 v[16:17], v[14:15], v[20:21], v[16:17] op_sel_hi:[1,0,1]
	s_nop 0
	v_pk_mul_f32 v[20:21], v[18:19], v[16:17] op_sel:[1,1] op_sel_hi:[1,0] neg_lo:[1,0]
	s_nop 0
	v_pk_fma_f32 v[18:19], v[18:19], v[16:17], v[20:21] op_sel_hi:[0,1,1]
	v_pk_mul_f32 v[20:21], v[14:15], v[16:17] op_sel:[1,1] op_sel_hi:[0,1] neg_lo:[0,1]
	v_pk_fma_f32 v[14:15], v[14:15], v[16:17], v[20:21] op_sel_hi:[1,0,1]
	s_nop 0
	v_pk_mul_f32 v[16:17], v[34:35], v[14:15] op_sel:[1,1] op_sel_hi:[1,0] neg_lo:[1,0]
	s_nop 0
	v_pk_fma_f32 v[14:15], v[34:35], v[14:15], v[16:17] op_sel_hi:[0,1,1]
	ds_write2_b64 v13, v[18:19], v[14:15] offset0:224 offset1:240
	v_mov_b32_e32 v14, v182
	v_mov_b32_e32 v10, v176
	v_mov_b32_e32 v13, v175
	s_waitcnt lgkmcnt(0)
	s_barrier
	v_mov_b32_e32 v48, v167
	v_xor_b32_e32 v16, 1, v13
	v_lshlrev_b32_e32 v10, 3, v10
	v_lshlrev_b32_e32 v16, 3, v16
	v_add3_u32 v18, 0, v16, v10
	v_xor_b32_e32 v16, 2, v13
	v_lshlrev_b32_e32 v16, 3, v16
	v_xor_b32_e32 v24, 5, v13
	v_add3_u32 v20, 0, v16, v10
	v_xor_b32_e32 v16, 3, v13
	v_lshlrev_b32_e32 v24, 3, v24
	v_lshlrev_b32_e32 v15, 3, v13
	v_lshlrev_b32_e32 v16, 3, v16
	v_add3_u32 v26, 0, v24, v10
	v_xor_b32_e32 v24, 6, v13
	v_add3_u32 v15, 0, v15, v10
	v_add3_u32 v22, 0, v16, v10
	v_lshlrev_b32_e32 v24, 3, v24
	v_xor_b32_e32 v32, 9, v13
	ds_read_b64 v[16:17], v15
	ds_read_b64 v[18:19], v18
	ds_read_b64 v[20:21], v20
	ds_read_b64 v[22:23], v22
	v_xor_b32_e32 v15, 4, v13
	v_add3_u32 v28, 0, v24, v10
	v_xor_b32_e32 v24, 7, v13
	v_lshlrev_b32_e32 v32, 3, v32
	v_lshlrev_b32_e32 v15, 3, v15
	v_lshlrev_b32_e32 v24, 3, v24
	v_add3_u32 v34, 0, v32, v10
	v_xor_b32_e32 v32, 10, v13
	v_add3_u32 v15, 0, v15, v10
	v_add3_u32 v30, 0, v24, v10
	v_lshlrev_b32_e32 v32, 3, v32
	ds_read_b64 v[24:25], v15
	ds_read_b64 v[26:27], v26
	ds_read_b64 v[28:29], v28
	ds_read_b64 v[30:31], v30
	v_xor_b32_e32 v15, 8, v13
	v_add3_u32 v36, 0, v32, v10
	v_xor_b32_e32 v32, 11, v13
	v_lshlrev_b32_e32 v15, 3, v15
	v_lshlrev_b32_e32 v32, 3, v32
	v_xor_b32_e32 v40, 13, v13
	v_add3_u32 v15, 0, v15, v10
	v_add3_u32 v38, 0, v32, v10
	v_lshlrev_b32_e32 v40, 3, v40
	ds_read_b64 v[32:33], v15
	ds_read_b64 v[34:35], v34
	ds_read_b64 v[36:37], v36
	ds_read_b64 v[38:39], v38
	v_xor_b32_e32 v15, 12, v13
	v_add3_u32 v42, 0, v40, v10
	v_xor_b32_e32 v40, 14, v13
	v_xor_b32_e32 v13, 15, v13
	v_lshlrev_b32_e32 v15, 3, v15
	v_lshlrev_b32_e32 v40, 3, v40
	v_lshlrev_b32_e32 v13, 3, v13
	v_add3_u32 v15, 0, v15, v10
	v_add3_u32 v44, 0, v40, v10
	v_add3_u32 v10, 0, v13, v10
	ds_read_b64 v[40:41], v15
	ds_read_b64 v[42:43], v42
	ds_read_b64 v[44:45], v44
	ds_read_b64 v[46:47], v10
	s_waitcnt lgkmcnt(7)
	v_pk_add_f32 v[52:53], v[16:17], v[32:33]
	v_mov_b32_e32 v10, v165
	v_pk_add_f32 v[16:17], v[16:17], v[32:33] neg_lo:[0,1] neg_hi:[0,1]
	s_waitcnt lgkmcnt(6)
	v_pk_add_f32 v[32:33], v[18:19], v[34:35]
	v_pk_add_f32 v[18:19], v[18:19], v[34:35] neg_lo:[0,1] neg_hi:[0,1]
	v_mov_b32_e32 v50, v169
	v_ashrrev_i32_e32 v15, 31, v14
	v_pk_mul_f32 v[34:35], v[18:19], v[50:51] op_sel:[1,0] op_sel_hi:[0,0] neg_lo:[1,1] neg_hi:[0,1]
	v_pk_fma_f32 v[18:19], v[18:19], v[10:11], v[34:35] op_sel_hi:[1,0,1]
	s_waitcnt lgkmcnt(5)
	v_pk_add_f32 v[34:35], v[20:21], v[36:37]
	v_pk_add_f32 v[20:21], v[20:21], v[36:37] neg_lo:[0,1] neg_hi:[0,1]
	s_nop 0
	v_pk_mul_f32 v[36:37], v[20:21], v[48:49] op_sel:[1,0] op_sel_hi:[0,0] neg_lo:[1,1] neg_hi:[0,1]
	v_pk_fma_f32 v[20:21], v[20:21], v[48:49], v[36:37] op_sel_hi:[1,0,1]
	s_waitcnt lgkmcnt(4)
	v_pk_add_f32 v[36:37], v[22:23], v[38:39]
	v_pk_add_f32 v[22:23], v[22:23], v[38:39] neg_lo:[0,1] neg_hi:[0,1]
	s_nop 0
	v_pk_mul_f32 v[38:39], v[22:23], v[50:51] op_sel_hi:[1,0]
	s_nop 0
	v_pk_fma_f32 v[22:23], v[22:23], v[10:11], v[38:39] op_sel:[1,0,0] op_sel_hi:[0,0,1] neg_lo:[1,1,0] neg_hi:[0,1,0]
	s_waitcnt lgkmcnt(3)
	v_pk_add_f32 v[38:39], v[24:25], v[40:41]
	v_pk_add_f32 v[24:25], v[24:25], v[40:41] neg_lo:[0,1] neg_hi:[0,1]
	v_mov_b32_e32 v13, v175
	v_xor_b32_e32 v41, 0x80000000, v24
	v_mov_b32_e32 v40, v25
	s_waitcnt lgkmcnt(2)
	v_pk_add_f32 v[24:25], v[26:27], v[42:43]
	v_pk_add_f32 v[26:27], v[26:27], v[42:43] neg_lo:[0,1] neg_hi:[0,1]
	s_nop 0
	v_pk_mul_f32 v[42:43], v[26:27], v[50:51] op_sel_hi:[1,0] neg_lo:[0,1] neg_hi:[0,1]
	s_nop 0
	v_pk_fma_f32 v[26:27], v[26:27], v[10:11], v[42:43] op_sel:[1,0,0] op_sel_hi:[0,0,1] neg_lo:[1,1,0] neg_hi:[0,1,0]
	s_waitcnt lgkmcnt(1)
	v_pk_add_f32 v[42:43], v[28:29], v[44:45]
	v_pk_add_f32 v[28:29], v[28:29], v[44:45] neg_lo:[0,1] neg_hi:[0,1]
	s_nop 0
	v_pk_mul_f32 v[44:45], v[28:29], v[48:49] op_sel:[1,0] op_sel_hi:[0,0] neg_lo:[1,1] neg_hi:[0,1]
	s_nop 0
	v_pk_fma_f32 v[28:29], v[28:29], v[48:49], v[44:45] op_sel_hi:[1,0,1] neg_lo:[0,1,0] neg_hi:[0,1,0]
	s_waitcnt lgkmcnt(0)
	v_pk_add_f32 v[44:45], v[30:31], v[46:47]
	v_pk_add_f32 v[30:31], v[30:31], v[46:47] neg_lo:[0,1] neg_hi:[0,1]
	s_nop 0
	v_pk_mul_f32 v[46:47], v[30:31], v[50:51] op_sel:[1,0] op_sel_hi:[0,0] neg_lo:[1,1] neg_hi:[0,1]
	v_pk_add_f32 v[50:51], v[32:33], v[24:25]
	v_pk_add_f32 v[24:25], v[32:33], v[24:25] neg_lo:[0,1] neg_hi:[0,1]
	v_pk_fma_f32 v[30:31], v[30:31], v[10:11], v[46:47] op_sel_hi:[1,0,1] neg_lo:[0,1,0] neg_hi:[0,1,0]
	v_pk_mul_f32 v[32:33], v[24:25], v[48:49] op_sel:[1,0] op_sel_hi:[0,0] neg_lo:[1,1] neg_hi:[0,1]
	v_pk_add_f32 v[46:47], v[52:53], v[38:39]
	v_pk_fma_f32 v[24:25], v[24:25], v[48:49], v[32:33] op_sel_hi:[1,0,1]
	v_pk_add_f32 v[32:33], v[34:35], v[42:43]
	v_pk_add_f32 v[34:35], v[34:35], v[42:43] neg_lo:[0,1] neg_hi:[0,1]
	v_pk_add_f32 v[38:39], v[52:53], v[38:39] neg_lo:[0,1] neg_hi:[0,1]
	v_xor_b32_e32 v43, 0x80000000, v34
	v_mov_b32_e32 v42, v35
	v_pk_add_f32 v[34:35], v[36:37], v[44:45]
	v_pk_add_f32 v[36:37], v[36:37], v[44:45] neg_lo:[0,1] neg_hi:[0,1]
	v_mov_b32_e32 v10, v177
	v_pk_mul_f32 v[44:45], v[36:37], v[48:49] op_sel:[1,0] op_sel_hi:[0,0] neg_lo:[1,1] neg_hi:[0,1]
	s_nop 0
	v_pk_fma_f32 v[36:37], v[36:37], v[48:49], v[44:45] op_sel_hi:[1,0,1] neg_lo:[0,1,0] neg_hi:[0,1,0]
	v_pk_add_f32 v[44:45], v[46:47], v[32:33]
	v_pk_add_f32 v[32:33], v[46:47], v[32:33] neg_lo:[0,1] neg_hi:[0,1]
	v_pk_add_f32 v[46:47], v[50:51], v[34:35]
	v_pk_add_f32 v[34:35], v[50:51], v[34:35] neg_lo:[0,1] neg_hi:[0,1]
	s_nop 0
	v_xor_b32_e32 v51, 0x80000000, v34
	v_mov_b32_e32 v50, v35
	v_pk_add_f32 v[34:35], v[44:45], v[46:47]
	v_pk_add_f32 v[44:45], v[44:45], v[46:47] neg_lo:[0,1] neg_hi:[0,1]
	v_pk_add_f32 v[46:47], v[32:33], v[50:51]
	v_pk_add_f32 v[32:33], v[32:33], v[50:51] neg_lo:[0,1] neg_hi:[0,1]
	v_pk_add_f32 v[50:51], v[38:39], v[42:43]
	v_pk_add_f32 v[38:39], v[38:39], v[42:43] neg_lo:[0,1] neg_hi:[0,1]
	v_pk_add_f32 v[42:43], v[24:25], v[36:37]
	v_pk_add_f32 v[24:25], v[24:25], v[36:37] neg_lo:[0,1] neg_hi:[0,1]
	s_nop 0
	v_xor_b32_e32 v37, 0x80000000, v24
	v_mov_b32_e32 v36, v25
	v_pk_add_f32 v[24:25], v[50:51], v[42:43]
	v_pk_add_f32 v[42:43], v[50:51], v[42:43] neg_lo:[0,1] neg_hi:[0,1]
	v_pk_add_f32 v[50:51], v[38:39], v[36:37]
	v_pk_add_f32 v[36:37], v[38:39], v[36:37] neg_lo:[0,1] neg_hi:[0,1]
	v_pk_add_f32 v[38:39], v[16:17], v[40:41]
	v_pk_add_f32 v[16:17], v[16:17], v[40:41] neg_lo:[0,1] neg_hi:[0,1]
	v_pk_add_f32 v[40:41], v[18:19], v[26:27]
	v_pk_add_f32 v[18:19], v[18:19], v[26:27] neg_lo:[0,1] neg_hi:[0,1]
	s_nop 0
	v_pk_mul_f32 v[26:27], v[48:49], v[18:19] op_sel:[0,1] op_sel_hi:[0,0] neg_lo:[1,1] neg_hi:[1,0]
	v_pk_fma_f32 v[18:19], v[48:49], v[18:19], v[26:27] op_sel_hi:[0,1,1]
	v_pk_add_f32 v[26:27], v[20:21], v[28:29]
	v_pk_add_f32 v[20:21], v[20:21], v[28:29] neg_lo:[0,1] neg_hi:[0,1]
	s_nop 0
	v_xor_b32_e32 v29, 0x80000000, v20
	v_mov_b32_e32 v28, v21
	v_pk_add_f32 v[20:21], v[22:23], v[30:31]
	v_pk_add_f32 v[22:23], v[22:23], v[30:31] neg_lo:[0,1] neg_hi:[0,1]
	s_nop 0
	v_pk_mul_f32 v[30:31], v[48:49], v[22:23] op_sel:[0,1] op_sel_hi:[0,0] neg_lo:[1,1] neg_hi:[1,0]
	v_pk_fma_f32 v[22:23], v[48:49], v[22:23], v[30:31] op_sel_hi:[0,1,1] neg_lo:[1,0,0] neg_hi:[1,0,0]
	v_pk_add_f32 v[30:31], v[38:39], v[26:27]
	v_pk_add_f32 v[26:27], v[38:39], v[26:27] neg_lo:[0,1] neg_hi:[0,1]
	v_pk_add_f32 v[38:39], v[40:41], v[20:21]
	v_pk_add_f32 v[20:21], v[40:41], v[20:21] neg_lo:[0,1] neg_hi:[0,1]
	v_mov_b32_e32 v48, v167
	v_xor_b32_e32 v41, 0x80000000, v20
	v_mov_b32_e32 v40, v21
	v_pk_add_f32 v[20:21], v[30:31], v[38:39]
	v_pk_add_f32 v[30:31], v[30:31], v[38:39] neg_lo:[0,1] neg_hi:[0,1]
	v_pk_add_f32 v[38:39], v[26:27], v[40:41]
	v_pk_add_f32 v[26:27], v[26:27], v[40:41] neg_lo:[0,1] neg_hi:[0,1]
	v_pk_add_f32 v[40:41], v[16:17], v[28:29]
	v_pk_add_f32 v[16:17], v[16:17], v[28:29] neg_lo:[0,1] neg_hi:[0,1]
	v_pk_add_f32 v[28:29], v[18:19], v[22:23]
	v_pk_add_f32 v[18:19], v[18:19], v[22:23] neg_lo:[0,1] neg_hi:[0,1]
	s_nop 0
	v_xor_b32_e32 v23, 0x80000000, v18
	v_mov_b32_e32 v22, v19
	v_pk_add_f32 v[18:19], v[40:41], v[28:29]
	v_pk_add_f32 v[28:29], v[40:41], v[28:29] neg_lo:[0,1] neg_hi:[0,1]
	v_pk_add_f32 v[40:41], v[16:17], v[22:23]
	v_pk_add_f32 v[16:17], v[16:17], v[22:23] neg_lo:[0,1] neg_hi:[0,1]
	v_lshl_add_u64 v[22:23], v[14:15], 3, s[46:47]
	global_store_dwordx2 v[22:23], v[34:35], off
	v_add_u32_e32 v22, 0x200, v14
	v_ashrrev_i32_e32 v23, 31, v22
	v_lshl_add_u64 v[22:23], v[22:23], 3, s[46:47]
	global_store_dwordx2 v[22:23], v[20:21], off
	v_add_u32_e32 v20, 0x400, v14
	v_ashrrev_i32_e32 v21, 31, v20
	v_lshl_add_u64 v[20:21], v[20:21], 3, s[46:47]
	global_store_dwordx2 v[20:21], v[24:25], off
	v_add_u32_e32 v20, 0x600, v14
	v_ashrrev_i32_e32 v21, 31, v20
	v_lshl_add_u64 v[20:21], v[20:21], 3, s[46:47]
	global_store_dwordx2 v[20:21], v[18:19], off
	v_add_u32_e32 v18, 0x800, v14
	v_ashrrev_i32_e32 v19, 31, v18
	v_lshl_add_u64 v[18:19], v[18:19], 3, s[46:47]
	global_store_dwordx2 v[18:19], v[46:47], off
	v_add_u32_e32 v18, 0xa00, v14
	v_ashrrev_i32_e32 v19, 31, v18
	v_lshl_add_u64 v[18:19], v[18:19], 3, s[46:47]
	global_store_dwordx2 v[18:19], v[38:39], off
	v_add_u32_e32 v18, 0xc00, v14
	v_ashrrev_i32_e32 v19, 31, v18
	v_lshl_add_u64 v[18:19], v[18:19], 3, s[46:47]
	global_store_dwordx2 v[18:19], v[50:51], off
	v_add_u32_e32 v18, 0xe00, v14
	v_ashrrev_i32_e32 v19, 31, v18
	v_lshl_add_u64 v[18:19], v[18:19], 3, s[46:47]
	global_store_dwordx2 v[18:19], v[40:41], off
	v_add_u32_e32 v18, 0x1000, v14
	v_ashrrev_i32_e32 v19, 31, v18
	v_lshl_add_u64 v[18:19], v[18:19], 3, s[46:47]
	global_store_dwordx2 v[18:19], v[44:45], off
	v_add_u32_e32 v18, 0x1200, v14
	v_ashrrev_i32_e32 v19, 31, v18
	v_lshl_add_u64 v[18:19], v[18:19], 3, s[46:47]
	global_store_dwordx2 v[18:19], v[30:31], off
	v_add_u32_e32 v18, 0x1400, v14
	v_ashrrev_i32_e32 v19, 31, v18
	v_lshl_add_u64 v[18:19], v[18:19], 3, s[46:47]
	global_store_dwordx2 v[18:19], v[42:43], off
	v_add_u32_e32 v18, 0x1600, v14
	v_ashrrev_i32_e32 v19, 31, v18
	v_lshl_add_u64 v[18:19], v[18:19], 3, s[46:47]
	global_store_dwordx2 v[18:19], v[28:29], off
	v_add_u32_e32 v18, 0x1800, v14
	v_ashrrev_i32_e32 v19, 31, v18
	v_lshl_add_u64 v[18:19], v[18:19], 3, s[46:47]
	global_store_dwordx2 v[18:19], v[32:33], off
	v_add_u32_e32 v18, 0x1a00, v14
	v_ashrrev_i32_e32 v19, 31, v18
	v_lshl_add_u64 v[18:19], v[18:19], 3, s[46:47]
	global_store_dwordx2 v[18:19], v[26:27], off
	v_add_u32_e32 v18, 0x1c00, v14
	v_ashrrev_i32_e32 v19, 31, v18
	v_lshl_add_u64 v[18:19], v[18:19], 3, s[46:47]
	global_store_dwordx2 v[18:19], v[36:37], off
	v_add_u32_e32 v18, 0x1e00, v14
	v_ashrrev_i32_e32 v19, 31, v18
	v_lshl_add_u64 v[18:19], v[18:19], 3, s[46:47]
	global_store_dwordx2 v[18:19], v[16:17], off
	v_mov_b32_e32 v50, v169
	v_xor_b32_e32 v16, 1, v13
	v_lshlrev_b32_e32 v10, 3, v10
	v_lshlrev_b32_e32 v16, 3, v16
	v_add3_u32 v18, 0, v16, v10
	v_xor_b32_e32 v16, 2, v13
	v_lshlrev_b32_e32 v16, 3, v16
	v_xor_b32_e32 v24, 5, v13
	v_add3_u32 v20, 0, v16, v10
	v_xor_b32_e32 v16, 3, v13
	v_lshlrev_b32_e32 v24, 3, v24
	v_lshlrev_b32_e32 v15, 3, v13
	v_lshlrev_b32_e32 v16, 3, v16
	v_add3_u32 v26, 0, v24, v10
	v_xor_b32_e32 v24, 6, v13
	v_add3_u32 v15, 0, v15, v10
	v_add3_u32 v22, 0, v16, v10
	v_lshlrev_b32_e32 v24, 3, v24
	v_xor_b32_e32 v32, 9, v13
	ds_read_b64 v[16:17], v15
	ds_read_b64 v[18:19], v18
	ds_read_b64 v[20:21], v20
	ds_read_b64 v[22:23], v22
	v_xor_b32_e32 v15, 4, v13
	v_add3_u32 v28, 0, v24, v10
	v_xor_b32_e32 v24, 7, v13
	v_lshlrev_b32_e32 v32, 3, v32
	v_lshlrev_b32_e32 v15, 3, v15
	v_lshlrev_b32_e32 v24, 3, v24
	v_add3_u32 v34, 0, v32, v10
	v_xor_b32_e32 v32, 10, v13
	v_add3_u32 v15, 0, v15, v10
	v_add3_u32 v30, 0, v24, v10
	v_lshlrev_b32_e32 v32, 3, v32
	ds_read_b64 v[24:25], v15
	ds_read_b64 v[26:27], v26
	ds_read_b64 v[28:29], v28
	ds_read_b64 v[30:31], v30
	v_xor_b32_e32 v15, 8, v13
	v_add3_u32 v36, 0, v32, v10
	v_xor_b32_e32 v32, 11, v13
	v_lshlrev_b32_e32 v15, 3, v15
	v_lshlrev_b32_e32 v32, 3, v32
	v_xor_b32_e32 v40, 13, v13
	v_add3_u32 v15, 0, v15, v10
	v_add3_u32 v38, 0, v32, v10
	v_lshlrev_b32_e32 v40, 3, v40
	ds_read_b64 v[32:33], v15
	ds_read_b64 v[34:35], v34
	ds_read_b64 v[36:37], v36
	ds_read_b64 v[38:39], v38
	v_xor_b32_e32 v15, 12, v13
	v_add3_u32 v42, 0, v40, v10
	v_xor_b32_e32 v40, 14, v13
	v_xor_b32_e32 v13, 15, v13
	v_lshlrev_b32_e32 v15, 3, v15
	v_lshlrev_b32_e32 v40, 3, v40
	v_lshlrev_b32_e32 v13, 3, v13
	v_add3_u32 v15, 0, v15, v10
	v_add3_u32 v44, 0, v40, v10
	v_add3_u32 v10, 0, v13, v10
	ds_read_b64 v[40:41], v15
	ds_read_b64 v[42:43], v42
	ds_read_b64 v[44:45], v44
	ds_read_b64 v[46:47], v10
	s_waitcnt lgkmcnt(7)
	v_pk_add_f32 v[52:53], v[16:17], v[32:33]
	v_mov_b32_e32 v10, v165
	v_pk_add_f32 v[16:17], v[16:17], v[32:33] neg_lo:[0,1] neg_hi:[0,1]
	s_waitcnt lgkmcnt(6)
	v_pk_add_f32 v[32:33], v[18:19], v[34:35]
	v_pk_add_f32 v[18:19], v[18:19], v[34:35] neg_lo:[0,1] neg_hi:[0,1]
	s_nop 0
	v_pk_mul_f32 v[34:35], v[18:19], v[50:51] op_sel:[1,0] op_sel_hi:[0,0] neg_lo:[1,1] neg_hi:[0,1]
	v_pk_fma_f32 v[18:19], v[18:19], v[10:11], v[34:35] op_sel_hi:[1,0,1]
	s_waitcnt lgkmcnt(5)
	v_pk_add_f32 v[34:35], v[20:21], v[36:37]
	v_pk_add_f32 v[20:21], v[20:21], v[36:37] neg_lo:[0,1] neg_hi:[0,1]
	s_nop 0
	v_pk_mul_f32 v[36:37], v[20:21], v[48:49] op_sel:[1,0] op_sel_hi:[0,0] neg_lo:[1,1] neg_hi:[0,1]
	v_pk_fma_f32 v[20:21], v[20:21], v[48:49], v[36:37] op_sel_hi:[1,0,1]
	s_waitcnt lgkmcnt(4)
	v_pk_add_f32 v[36:37], v[22:23], v[38:39]
	v_pk_add_f32 v[22:23], v[22:23], v[38:39] neg_lo:[0,1] neg_hi:[0,1]
	s_nop 0
	v_pk_mul_f32 v[38:39], v[22:23], v[50:51] op_sel_hi:[1,0]
	s_nop 0
	v_pk_fma_f32 v[22:23], v[22:23], v[10:11], v[38:39] op_sel:[1,0,0] op_sel_hi:[0,0,1] neg_lo:[1,1,0] neg_hi:[0,1,0]
	s_waitcnt lgkmcnt(3)
	v_pk_add_f32 v[38:39], v[24:25], v[40:41]
	v_pk_add_f32 v[24:25], v[24:25], v[40:41] neg_lo:[0,1] neg_hi:[0,1]
	v_mov_b32_e32 v13, v173
	v_xor_b32_e32 v41, 0x80000000, v24
	v_mov_b32_e32 v40, v25
	s_waitcnt lgkmcnt(2)
	v_pk_add_f32 v[24:25], v[26:27], v[42:43]
	v_pk_add_f32 v[26:27], v[26:27], v[42:43] neg_lo:[0,1] neg_hi:[0,1]
	s_nop 0
	v_pk_mul_f32 v[42:43], v[26:27], v[50:51] op_sel_hi:[1,0] neg_lo:[0,1] neg_hi:[0,1]
	s_nop 0
	v_pk_fma_f32 v[26:27], v[26:27], v[10:11], v[42:43] op_sel:[1,0,0] op_sel_hi:[0,0,1] neg_lo:[1,1,0] neg_hi:[0,1,0]
	s_waitcnt lgkmcnt(1)
	v_pk_add_f32 v[42:43], v[28:29], v[44:45]
	v_pk_add_f32 v[28:29], v[28:29], v[44:45] neg_lo:[0,1] neg_hi:[0,1]
	s_nop 0
	v_pk_mul_f32 v[44:45], v[28:29], v[48:49] op_sel:[1,0] op_sel_hi:[0,0] neg_lo:[1,1] neg_hi:[0,1]
	s_nop 0
	v_pk_fma_f32 v[28:29], v[28:29], v[48:49], v[44:45] op_sel_hi:[1,0,1] neg_lo:[0,1,0] neg_hi:[0,1,0]
	s_waitcnt lgkmcnt(0)
	v_pk_add_f32 v[44:45], v[30:31], v[46:47]
	v_pk_add_f32 v[30:31], v[30:31], v[46:47] neg_lo:[0,1] neg_hi:[0,1]
	s_nop 0
	v_pk_mul_f32 v[46:47], v[30:31], v[50:51] op_sel:[1,0] op_sel_hi:[0,0] neg_lo:[1,1] neg_hi:[0,1]
	v_pk_add_f32 v[50:51], v[32:33], v[24:25]
	v_pk_add_f32 v[24:25], v[32:33], v[24:25] neg_lo:[0,1] neg_hi:[0,1]
	v_pk_fma_f32 v[30:31], v[30:31], v[10:11], v[46:47] op_sel_hi:[1,0,1] neg_lo:[0,1,0] neg_hi:[0,1,0]
	v_pk_mul_f32 v[32:33], v[24:25], v[48:49] op_sel:[1,0] op_sel_hi:[0,0] neg_lo:[1,1] neg_hi:[0,1]
	v_pk_add_f32 v[46:47], v[52:53], v[38:39]
	v_pk_fma_f32 v[24:25], v[24:25], v[48:49], v[32:33] op_sel_hi:[1,0,1]
	v_pk_add_f32 v[32:33], v[34:35], v[42:43]
	v_pk_add_f32 v[34:35], v[34:35], v[42:43] neg_lo:[0,1] neg_hi:[0,1]
	v_pk_add_f32 v[38:39], v[52:53], v[38:39] neg_lo:[0,1] neg_hi:[0,1]
	v_xor_b32_e32 v43, 0x80000000, v34
	v_mov_b32_e32 v42, v35
	v_pk_add_f32 v[34:35], v[36:37], v[44:45]
	v_pk_add_f32 v[36:37], v[36:37], v[44:45] neg_lo:[0,1] neg_hi:[0,1]
	v_mov_b32_e32 v10, v183
	v_pk_mul_f32 v[44:45], v[36:37], v[48:49] op_sel:[1,0] op_sel_hi:[0,0] neg_lo:[1,1] neg_hi:[0,1]
	s_nop 0
	v_pk_fma_f32 v[36:37], v[36:37], v[48:49], v[44:45] op_sel_hi:[1,0,1] neg_lo:[0,1,0] neg_hi:[0,1,0]
	v_pk_add_f32 v[44:45], v[46:47], v[32:33]
	v_pk_add_f32 v[32:33], v[46:47], v[32:33] neg_lo:[0,1] neg_hi:[0,1]
	v_pk_add_f32 v[46:47], v[50:51], v[34:35]
	v_pk_add_f32 v[34:35], v[50:51], v[34:35] neg_lo:[0,1] neg_hi:[0,1]
	s_nop 0
	v_xor_b32_e32 v51, 0x80000000, v34
	v_mov_b32_e32 v50, v35
	v_pk_add_f32 v[34:35], v[44:45], v[46:47]
	v_pk_add_f32 v[44:45], v[44:45], v[46:47] neg_lo:[0,1] neg_hi:[0,1]
	v_pk_add_f32 v[46:47], v[32:33], v[50:51]
	v_pk_add_f32 v[32:33], v[32:33], v[50:51] neg_lo:[0,1] neg_hi:[0,1]
	v_pk_add_f32 v[50:51], v[38:39], v[42:43]
	v_pk_add_f32 v[38:39], v[38:39], v[42:43] neg_lo:[0,1] neg_hi:[0,1]
	v_pk_add_f32 v[42:43], v[24:25], v[36:37]
	v_pk_add_f32 v[24:25], v[24:25], v[36:37] neg_lo:[0,1] neg_hi:[0,1]
	s_nop 0
	v_xor_b32_e32 v37, 0x80000000, v24
	v_mov_b32_e32 v36, v25
	v_pk_add_f32 v[24:25], v[50:51], v[42:43]
	v_pk_add_f32 v[42:43], v[50:51], v[42:43] neg_lo:[0,1] neg_hi:[0,1]
	v_pk_add_f32 v[50:51], v[38:39], v[36:37]
	v_pk_add_f32 v[36:37], v[38:39], v[36:37] neg_lo:[0,1] neg_hi:[0,1]
	v_pk_add_f32 v[38:39], v[16:17], v[40:41]
	v_pk_add_f32 v[16:17], v[16:17], v[40:41] neg_lo:[0,1] neg_hi:[0,1]
	v_pk_add_f32 v[40:41], v[18:19], v[26:27]
	v_pk_add_f32 v[18:19], v[18:19], v[26:27] neg_lo:[0,1] neg_hi:[0,1]
	s_nop 0
	v_pk_mul_f32 v[26:27], v[48:49], v[18:19] op_sel:[0,1] op_sel_hi:[0,0] neg_lo:[1,1] neg_hi:[1,0]
	v_pk_fma_f32 v[18:19], v[48:49], v[18:19], v[26:27] op_sel_hi:[0,1,1]
	v_pk_add_f32 v[26:27], v[20:21], v[28:29]
	v_pk_add_f32 v[20:21], v[20:21], v[28:29] neg_lo:[0,1] neg_hi:[0,1]
	s_nop 0
	v_xor_b32_e32 v29, 0x80000000, v20
	v_mov_b32_e32 v28, v21
	v_pk_add_f32 v[20:21], v[22:23], v[30:31]
	v_pk_add_f32 v[22:23], v[22:23], v[30:31] neg_lo:[0,1] neg_hi:[0,1]
	s_nop 0
	v_pk_mul_f32 v[30:31], v[48:49], v[22:23] op_sel:[0,1] op_sel_hi:[0,0] neg_lo:[1,1] neg_hi:[1,0]
	v_pk_fma_f32 v[22:23], v[48:49], v[22:23], v[30:31] op_sel_hi:[0,1,1] neg_lo:[1,0,0] neg_hi:[1,0,0]
	v_pk_add_f32 v[30:31], v[38:39], v[26:27]
	v_pk_add_f32 v[26:27], v[38:39], v[26:27] neg_lo:[0,1] neg_hi:[0,1]
	v_pk_add_f32 v[38:39], v[40:41], v[20:21]
	v_pk_add_f32 v[20:21], v[40:41], v[20:21] neg_lo:[0,1] neg_hi:[0,1]
	s_nop 0
	v_xor_b32_e32 v41, 0x80000000, v20
	v_mov_b32_e32 v40, v21
	v_pk_add_f32 v[20:21], v[30:31], v[38:39]
	v_pk_add_f32 v[30:31], v[30:31], v[38:39] neg_lo:[0,1] neg_hi:[0,1]
	v_pk_add_f32 v[38:39], v[26:27], v[40:41]
	v_pk_add_f32 v[26:27], v[26:27], v[40:41] neg_lo:[0,1] neg_hi:[0,1]
	v_pk_add_f32 v[40:41], v[16:17], v[28:29]
	v_pk_add_f32 v[16:17], v[16:17], v[28:29] neg_lo:[0,1] neg_hi:[0,1]
	v_pk_add_f32 v[28:29], v[18:19], v[22:23]
	v_pk_add_f32 v[18:19], v[18:19], v[22:23] neg_lo:[0,1] neg_hi:[0,1]
	s_nop 0
	v_xor_b32_e32 v23, 0x80000000, v18
	v_mov_b32_e32 v22, v19
	v_pk_add_f32 v[18:19], v[40:41], v[28:29]
	v_pk_add_f32 v[28:29], v[40:41], v[28:29] neg_lo:[0,1] neg_hi:[0,1]
	v_pk_add_f32 v[40:41], v[16:17], v[22:23]
	v_pk_add_f32 v[16:17], v[16:17], v[22:23] neg_lo:[0,1] neg_hi:[0,1]
	v_add_u32_e32 v22, 0x2000, v14
	v_ashrrev_i32_e32 v23, 31, v22
	v_lshl_add_u64 v[22:23], v[22:23], 3, s[46:47]
	global_store_dwordx2 v[22:23], v[34:35], off
	v_add_u32_e32 v22, 0x2200, v14
	v_ashrrev_i32_e32 v23, 31, v22
	v_lshl_add_u64 v[22:23], v[22:23], 3, s[46:47]
	global_store_dwordx2 v[22:23], v[20:21], off
	v_add_u32_e32 v20, 0x2400, v14
	v_ashrrev_i32_e32 v21, 31, v20
	v_lshl_add_u64 v[20:21], v[20:21], 3, s[46:47]
	global_store_dwordx2 v[20:21], v[24:25], off
	v_add_u32_e32 v20, 0x2600, v14
	v_ashrrev_i32_e32 v21, 31, v20
	v_lshl_add_u64 v[20:21], v[20:21], 3, s[46:47]
	global_store_dwordx2 v[20:21], v[18:19], off
	v_add_u32_e32 v18, 0x2800, v14
	v_ashrrev_i32_e32 v19, 31, v18
	v_lshl_add_u64 v[18:19], v[18:19], 3, s[46:47]
	global_store_dwordx2 v[18:19], v[46:47], off
	v_add_u32_e32 v18, 0x2a00, v14
	v_ashrrev_i32_e32 v19, 31, v18
	v_lshl_add_u64 v[18:19], v[18:19], 3, s[46:47]
	global_store_dwordx2 v[18:19], v[38:39], off
	v_add_u32_e32 v18, 0x2c00, v14
	v_ashrrev_i32_e32 v19, 31, v18
	v_lshl_add_u64 v[18:19], v[18:19], 3, s[46:47]
	global_store_dwordx2 v[18:19], v[50:51], off
	v_add_u32_e32 v18, 0x2e00, v14
	v_ashrrev_i32_e32 v19, 31, v18
	v_lshl_add_u64 v[18:19], v[18:19], 3, s[46:47]
	global_store_dwordx2 v[18:19], v[40:41], off
	v_add_u32_e32 v18, 0x3000, v14
	v_ashrrev_i32_e32 v19, 31, v18
	v_lshl_add_u64 v[18:19], v[18:19], 3, s[46:47]
	global_store_dwordx2 v[18:19], v[44:45], off
	v_add_u32_e32 v18, 0x3200, v14
	v_ashrrev_i32_e32 v19, 31, v18
	v_lshl_add_u64 v[18:19], v[18:19], 3, s[46:47]
	global_store_dwordx2 v[18:19], v[30:31], off
	v_add_u32_e32 v18, 0x3400, v14
	v_ashrrev_i32_e32 v19, 31, v18
	v_lshl_add_u64 v[18:19], v[18:19], 3, s[46:47]
	global_store_dwordx2 v[18:19], v[42:43], off
	v_add_u32_e32 v18, 0x3600, v14
	v_ashrrev_i32_e32 v19, 31, v18
	v_lshl_add_u64 v[18:19], v[18:19], 3, s[46:47]
	global_store_dwordx2 v[18:19], v[28:29], off
	v_add_u32_e32 v18, 0x3800, v14
	v_ashrrev_i32_e32 v19, 31, v18
	v_lshl_add_u64 v[18:19], v[18:19], 3, s[46:47]
	global_store_dwordx2 v[18:19], v[32:33], off
	v_add_u32_e32 v18, 0x3a00, v14
	v_ashrrev_i32_e32 v19, 31, v18
	v_lshl_add_u64 v[18:19], v[18:19], 3, s[46:47]
	global_store_dwordx2 v[18:19], v[26:27], off
	v_add_u32_e32 v18, 0x3c00, v14
	v_add_u32_e32 v14, 0x3e00, v14
	v_ashrrev_i32_e32 v15, 31, v14
	v_ashrrev_i32_e32 v19, 31, v18
	v_lshl_add_u64 v[14:15], v[14:15], 3, s[46:47]
	v_lshl_add_u64 v[18:19], v[18:19], 3, s[46:47]
	global_store_dwordx2 v[14:15], v[16:17], off
	v_mov_b32_e32 v16, v184
	v_mov_b32_e32 v14, v182
	global_store_dwordx2 v[18:19], v[36:37], off
	s_barrier
	s_nop 0
	v_pk_mul_f32 v[36:37], v[16:17], s[64:65] op_sel_hi:[0,1] neg_lo:[1,0]
	s_mov_b64 s[64:65], vcc
	v_ashrrev_i32_e32 v15, 31, v14
	v_lshl_add_u64 v[18:19], v[14:15], 2, s[64:65]
	s_movk_i32 vcc_lo, 0x1000
	v_add_co_u32_e32 v28, vcc, vcc_lo, v18
	v_pk_mul_f32 v[40:41], v[16:17], s[78:79] op_sel_hi:[0,1] neg_lo:[1,0]
	s_nop 0
	v_addc_co_u32_e32 v29, vcc, 0, v19, vcc
	v_add_co_u32_e32 v20, vcc, s39, v18
	s_movk_i32 s78, 0x3000
	s_nop 0
	v_addc_co_u32_e32 v21, vcc, 0, v19, vcc
	v_add_co_u32_e32 v48, vcc, s78, v18
	v_pk_mul_f32 v[32:33], v[16:17], s[40:41] op_sel_hi:[0,1] neg_lo:[1,0]
	s_nop 0
	v_addc_co_u32_e32 v49, vcc, 0, v19, vcc
	v_add_co_u32_e32 v22, vcc, s72, v18
	s_mov_b32 s40, 0x3f7ec46d
	s_nop 0
	v_addc_co_u32_e32 v23, vcc, 0, v19, vcc
	v_add_co_u32_e32 v58, vcc, s33, v18
	s_mov_b32 s33, 0x8000
	s_nop 0
	v_addc_co_u32_e32 v59, vcc, 0, v19, vcc
	v_add_co_u32_e32 v60, vcc, s43, v18
	s_mov_b32 s41, 0xbdc8bd36
	s_nop 0
	v_addc_co_u32_e32 v61, vcc, 0, v19, vcc
	v_add_co_u32_e32 v64, vcc, s73, v18
	v_pk_mul_f32 v[34:35], v[16:17], s[76:77] op_sel_hi:[0,1] neg_lo:[1,0]
	s_nop 0
	v_addc_co_u32_e32 v65, vcc, 0, v19, vcc
	v_add_co_u32_e32 v68, vcc, s33, v18
	s_mov_b32 s33, 0x9000
	s_nop 0
	v_addc_co_u32_e32 v69, vcc, 0, v19, vcc
	v_add_co_u32_e32 v24, vcc, s33, v18
	s_mov_b32 s33, 0xa000
	s_nop 0
	v_addc_co_u32_e32 v25, vcc, 0, v19, vcc
	v_add_co_u32_e32 v26, vcc, s33, v18
	s_mov_b32 s33, 0xb000
	s_nop 0
	v_addc_co_u32_e32 v27, vcc, 0, v19, vcc
	v_add_co_u32_e32 v30, vcc, s33, v18
	s_mov_b32 s33, 0xc000
	s_nop 0
	v_addc_co_u32_e32 v31, vcc, 0, v19, vcc
	v_add_co_u32_e32 v38, vcc, s33, v18
	s_mov_b32 s33, 0xd000
	s_nop 0
	v_addc_co_u32_e32 v39, vcc, 0, v19, vcc
	v_add_co_u32_e32 v44, vcc, s33, v18
	s_mov_b32 s33, 0xe000
	s_nop 0
	v_addc_co_u32_e32 v45, vcc, 0, v19, vcc
	v_add_co_u32_e32 v50, vcc, s33, v18
	s_mov_b32 s33, 0xf000
	s_nop 0
	v_addc_co_u32_e32 v51, vcc, 0, v19, vcc
	v_add_co_u32_e32 v70, vcc, s33, v18
	v_pk_mul_f32 v[92:93], v[16:17], s[62:63] op_sel_hi:[0,1] neg_lo:[1,0]
	s_nop 0
	v_addc_co_u32_e32 v71, vcc, 0, v19, vcc
	global_load_dword v94, v[68:69], off
	global_load_dword v96, v[68:69], off offset:2048
	global_load_dword v98, v[26:27], off offset:-4096
	global_load_dword v100, v[24:25], off offset:2048
	global_load_dword v102, v[26:27], off
	global_load_dword v104, v[26:27], off offset:2048
	global_load_dword v106, v[38:39], off offset:-4096
	global_load_dword v108, v[30:31], off offset:2048
	global_load_dword v110, v[38:39], off
	global_load_dword v112, v[38:39], off offset:2048
	global_load_dword v114, v[50:51], off offset:-4096
	global_load_dword v116, v[44:45], off offset:2048
	global_load_dword v118, v[50:51], off
	global_load_dword v120, v[50:51], off offset:2048
	global_load_dword v122, v[70:71], off
	global_load_dword v56, v[20:21], off
	s_nop 0
	global_load_dword v50, v[20:21], off offset:2048
	global_load_dword v124, v[70:71], off offset:2048
	global_load_dword v44, v[22:23], off offset:-4096
	global_load_dword v38, v[22:23], off
	global_load_dword v72, v[20:21], off offset:-4096
	global_load_dword v30, v[22:23], off offset:2048
	global_load_dword v26, v[60:61], off offset:-4096
	global_load_dword v24, v[60:61], off
	s_nop 0
	global_load_dword v22, v[60:61], off offset:2048
	global_load_dword v20, v[68:69], off offset:-4096
	global_load_dword v74, v[18:19], off
	global_load_dword v78, v[18:19], off offset:2048
	s_nop 0
	global_load_dword v68, v[28:29], off offset:2048
	s_nop 0
	global_load_dword v48, v[48:49], off offset:2048
	s_nop 0
	global_load_dword v28, v[58:59], off offset:2048
	global_load_dword v18, v[64:65], off offset:2048
	v_pk_mul_f32 v[52:53], v[16:17], s[58:59] op_sel_hi:[0,1] neg_lo:[1,0]
	v_pk_fma_f32 v[82:83], v[10:11], s[40:41], v[34:35] op_sel_hi:[0,1,1]
	v_pk_fma_f32 v[34:35], v[10:11], s[92:93], v[92:93] op_sel_hi:[0,1,1]
	s_mov_b32 s92, 0x3e47c5c2
	v_pk_mul_f32 v[66:67], v[16:17], s[60:61] op_sel_hi:[0,1] neg_lo:[1,0]
	v_pk_fma_f32 v[84:85], v[10:11], s[44:45], v[32:33] op_sel_hi:[0,1,1]
	v_pk_fma_f32 v[60:61], v[10:11], s[82:83], v[52:53] op_sel_hi:[0,1,1]
	s_mov_b32 s82, 0x3f45e403
	s_mov_b32 s93, 0xbf7b14be
	v_pk_mul_f32 v[32:33], v[16:17], s[30:31] op_sel_hi:[0,1] neg_lo:[1,0]
	s_mov_b32 s30, 0x3dc8bd36
	v_pk_mul_f32 v[54:55], v[16:17], s[74:75] op_sel_hi:[0,1] neg_lo:[1,0]
	v_pk_mul_f32 v[62:63], v[16:17], s[54:55] op_sel_hi:[0,1] neg_lo:[1,0]
	s_mov_b32 s83, 0xbf226799
	v_pk_fma_f32 v[52:53], v[10:11], s[86:87], v[66:67] op_sel_hi:[0,1,1]
	s_mov_b32 s31, 0xbf7ec46d
	v_pk_fma_f32 v[66:67], v[10:11], s[92:93], v[32:33] op_sel_hi:[0,1,1]
	v_pk_mul_f32 v[32:33], v[16:17], s[34:35] op_sel_hi:[0,1] neg_lo:[1,0]
	v_pk_fma_f32 v[76:77], v[10:11], s[80:81], v[40:41] op_sel_hi:[0,1,1]
	s_mov_b32 s80, 0x3f61c598
	v_pk_fma_f32 v[58:59], v[10:11], s[82:83], v[54:55] op_sel_hi:[0,1,1]
	v_pk_fma_f32 v[54:55], v[10:11], s[84:85], v[62:63] op_sel_hi:[0,1,1]
	s_mov_b32 s86, 0x3f0e39da
	v_pk_fma_f32 v[62:63], v[10:11], s[30:31], v[32:33] op_sel_hi:[0,1,1]
	v_pk_mul_f32 v[32:33], v[16:17], s[36:37] op_sel_hi:[0,1] neg_lo:[1,0]
	v_pk_mul_f32 v[46:47], v[16:17], s[48:49] op_sel_hi:[0,1] neg_lo:[1,0]
	v_pk_mul_f32 v[86:87], v[16:17], s[66:67] op_sel_hi:[0,1] neg_lo:[1,0]
	s_mov_b32 s81, 0xbef15aea
	s_mov_b32 s87, 0xbf54db31
	v_pk_fma_f32 v[32:33], v[10:11], s[96:97], v[32:33] op_sel_hi:[0,1,1]
	s_mov_b32 s54, 0x3f6c835e
	v_pk_fma_f32 v[64:65], v[10:11], s[80:81], v[46:47] op_sel_hi:[0,1,1]
	v_pk_fma_f32 v[46:47], v[10:11], s[86:87], v[86:87] op_sel_hi:[0,1,1]
	v_pk_mul_f32 v[42:43], v[16:17], s[50:51] op_sel_hi:[0,1] neg_lo:[1,0]
	v_pk_mul_f32 v[88:89], v[16:17], s[68:69] op_sel_hi:[0,1] neg_lo:[1,0]
	s_mov_b32 s55, 0xbec3ef15
	v_pk_fma_f32 v[70:71], v[10:11], s[54:55], v[42:43] op_sel_hi:[0,1,1]
	v_pk_fma_f32 v[42:43], v[10:11], s[88:89], v[88:89] op_sel_hi:[0,1,1]
	s_mov_b32 s88, 0x3ec3ef15
	v_pk_mul_f32 v[90:91], v[16:17], s[56:57] op_sel_hi:[0,1] neg_lo:[1,0]
	s_mov_b32 s89, 0xbf6c835e
	v_pk_fma_f32 v[40:41], v[10:11], s[88:89], v[90:91] op_sel_hi:[0,1,1]
	s_mov_b32 s76, 0x3f7b14be
	s_mov_b32 s77, 0xbe47c5c2
	v_pk_fma_f32 v[80:81], v[10:11], s[76:77], v[36:37] op_sel_hi:[0,1,1]
	v_mov_b32_e32 v36, v169
	s_waitcnt vmcnt(31)
	v_pk_mul_f32 v[86:87], v[32:33], v[94:95] op_sel_hi:[1,0]
	v_pk_mul_f32 v[32:33], v[16:17], s[2:3] op_sel_hi:[0,1] neg_lo:[1,0]
	v_pk_fma_f32 v[32:33], v[10:11], s[0:1], v[32:33] op_sel_hi:[0,1,1]
	s_waitcnt vmcnt(30)
	v_pk_mul_f32 v[88:89], v[32:33], v[96:97] op_sel_hi:[1,0]
	v_pk_mul_f32 v[32:33], v[16:17], s[6:7] op_sel_hi:[0,1] neg_lo:[1,0]
	v_pk_fma_f32 v[32:33], v[10:11], s[4:5], v[32:33] op_sel_hi:[0,1,1]
	s_waitcnt vmcnt(29)
	v_pk_mul_f32 v[90:91], v[32:33], v[98:99] op_sel_hi:[1,0]
	v_pk_mul_f32 v[32:33], v[16:17], s[10:11] op_sel_hi:[0,1] neg_lo:[1,0]
	v_pk_fma_f32 v[32:33], v[10:11], s[8:9], v[32:33] op_sel_hi:[0,1,1]
	s_waitcnt vmcnt(28)
	v_pk_mul_f32 v[92:93], v[32:33], v[100:101] op_sel_hi:[1,0]
	v_pk_mul_f32 v[32:33], v[16:17], s[16:17] op_sel_hi:[0,1] neg_lo:[1,0]
	v_pk_fma_f32 v[32:33], v[10:11], s[12:13], v[32:33] op_sel_hi:[0,1,1]
	s_waitcnt vmcnt(27)
	v_pk_mul_f32 v[94:95], v[32:33], v[102:103] op_sel_hi:[1,0]
	v_pk_mul_f32 v[32:33], v[16:17], s[20:21] op_sel_hi:[0,1] neg_lo:[1,0]
	v_pk_fma_f32 v[32:33], v[10:11], s[18:19], v[32:33] op_sel_hi:[0,1,1]
	s_waitcnt vmcnt(26)
	v_pk_mul_f32 v[96:97], v[32:33], v[104:105] op_sel_hi:[1,0]
	v_pk_mul_f32 v[32:33], v[16:17], s[24:25] op_sel_hi:[0,1] neg_lo:[1,0]
	v_pk_fma_f32 v[32:33], v[10:11], s[22:23], v[32:33] op_sel_hi:[0,1,1]
	s_waitcnt vmcnt(25)
	v_pk_mul_f32 v[98:99], v[32:33], v[106:107] op_sel_hi:[1,0]
	v_pk_mul_f32 v[32:33], v[16:17], s[28:29] op_sel_hi:[0,1] neg_lo:[1,0]
	v_pk_fma_f32 v[32:33], v[10:11], s[26:27], v[32:33] op_sel_hi:[0,1,1]
	s_waitcnt vmcnt(24)
	v_pk_mul_f32 v[100:101], v[32:33], v[108:109] op_sel_hi:[1,0]
	v_pk_mul_f32 v[32:33], v[16:17], s[84:85] op_sel_hi:[0,0] neg_lo:[1,0]
	v_pk_fma_f32 v[32:33], v[10:11], s[38:39], v[32:33] op_sel_hi:[0,0,1] neg_lo:[0,0,1] neg_hi:[0,0,1]
	s_waitcnt vmcnt(23)
	v_pk_mul_f32 v[102:103], v[32:33], v[110:111] op_sel_hi:[1,0]
	v_pk_mul_f32 v[32:33], v[16:17], s[26:27] op_sel_hi:[0,1] neg_lo:[1,0]
	v_pk_fma_f32 v[32:33], v[10:11], s[28:29], v[32:33] op_sel_hi:[0,1,1]
	s_waitcnt vmcnt(22)
	v_pk_mul_f32 v[104:105], v[32:33], v[112:113] op_sel_hi:[1,0]
	v_pk_mul_f32 v[32:33], v[16:17], s[22:23] op_sel_hi:[0,1] neg_lo:[1,0]
	v_pk_fma_f32 v[32:33], v[10:11], s[24:25], v[32:33] op_sel_hi:[0,1,1]
	s_waitcnt vmcnt(21)
	v_pk_mul_f32 v[106:107], v[32:33], v[114:115] op_sel_hi:[1,0]
	v_pk_mul_f32 v[32:33], v[16:17], s[18:19] op_sel_hi:[0,1] neg_lo:[1,0]
	v_pk_fma_f32 v[32:33], v[10:11], s[20:21], v[32:33] op_sel_hi:[0,1,1]
	s_waitcnt vmcnt(20)
	v_pk_mul_f32 v[108:109], v[32:33], v[116:117] op_sel_hi:[1,0]
	v_pk_mul_f32 v[32:33], v[16:17], s[12:13] op_sel_hi:[0,1] neg_lo:[1,0]
	v_pk_fma_f32 v[32:33], v[10:11], s[16:17], v[32:33] op_sel_hi:[0,1,1]
	s_waitcnt vmcnt(19)
	v_pk_mul_f32 v[110:111], v[32:33], v[118:119] op_sel_hi:[1,0]
	v_pk_mul_f32 v[32:33], v[16:17], s[8:9] op_sel_hi:[0,1] neg_lo:[1,0]
	v_pk_fma_f32 v[32:33], v[10:11], s[10:11], v[32:33] op_sel_hi:[0,1,1]
	s_waitcnt vmcnt(18)
	v_pk_mul_f32 v[112:113], v[32:33], v[120:121] op_sel_hi:[1,0]
	v_pk_mul_f32 v[32:33], v[16:17], s[4:5] op_sel_hi:[0,1] neg_lo:[1,0]
	v_pk_mul_f32 v[16:17], v[16:17], s[0:1] op_sel_hi:[0,1] neg_lo:[1,0]
	v_pk_fma_f32 v[16:17], v[10:11], s[2:3], v[16:17] op_sel_hi:[0,1,1]
	v_pk_fma_f32 v[32:33], v[10:11], s[6:7], v[32:33] op_sel_hi:[0,1,1]
	s_waitcnt vmcnt(14)
	v_pk_mul_f32 v[116:117], v[16:17], v[124:125] op_sel_hi:[1,0]
	s_waitcnt vmcnt(5)
	v_pk_fma_f32 v[126:127], v[74:75], v[84:85], v[86:87] op_sel_hi:[0,1,1]
	v_pk_fma_f32 v[74:75], v[74:75], v[84:85], v[86:87] op_sel_hi:[0,1,1] neg_lo:[0,0,1] neg_hi:[0,0,1]
	s_waitcnt vmcnt(4)
	v_pk_fma_f32 v[84:85], v[82:83], v[78:79], v[88:89] op_sel_hi:[1,0,1]
	v_pk_fma_f32 v[78:79], v[82:83], v[78:79], v[88:89] op_sel_hi:[1,0,1] neg_lo:[0,0,1] neg_hi:[0,0,1]
	v_pk_mul_f32 v[114:115], v[32:33], v[122:123] op_sel_hi:[1,0]
	v_mov_b32_e32 v118, v164
	v_mov_b32_e32 v32, v165
	v_mov_b32_e32 v120, v166
	v_mov_b32_e32 v10, v167
	v_mov_b32_e32 v122, v168
	v_mov_b32_e32 v124, v170
	s_nop 0
	v_pk_mul_f32 v[82:83], v[78:79], v[124:125] op_sel:[1,0] op_sel_hi:[0,0] neg_lo:[1,1] neg_hi:[0,1]
	s_nop 0
	v_pk_fma_f32 v[78:79], v[78:79], v[118:119], v[82:83] op_sel_hi:[1,0,1]
	v_pk_fma_f32 v[82:83], v[80:81], v[72:73], v[90:91] op_sel_hi:[1,0,1]
	v_pk_fma_f32 v[72:73], v[80:81], v[72:73], v[90:91] op_sel_hi:[1,0,1] neg_lo:[0,0,1] neg_hi:[0,0,1]
	s_nop 0
	v_pk_mul_f32 v[80:81], v[72:73], v[36:37] op_sel:[1,0] op_sel_hi:[0,0] neg_lo:[1,1] neg_hi:[0,1]
	s_nop 0
	v_pk_fma_f32 v[72:73], v[72:73], v[32:33], v[80:81] op_sel_hi:[1,0,1]
	s_waitcnt vmcnt(3)
	v_pk_fma_f32 v[80:81], v[76:77], v[68:69], v[92:93] op_sel_hi:[1,0,1]
	v_pk_fma_f32 v[68:69], v[76:77], v[68:69], v[92:93] op_sel_hi:[1,0,1] neg_lo:[0,0,1] neg_hi:[0,0,1]
	s_nop 0
	v_pk_mul_f32 v[76:77], v[68:69], v[122:123] op_sel:[1,0] op_sel_hi:[0,0] neg_lo:[1,1] neg_hi:[0,1]
	s_nop 0
	v_pk_fma_f32 v[68:69], v[68:69], v[120:121], v[76:77] op_sel_hi:[1,0,1]
	v_pk_fma_f32 v[76:77], v[70:71], v[56:57], v[94:95] op_sel_hi:[1,0,1]
	v_pk_fma_f32 v[56:57], v[70:71], v[56:57], v[94:95] op_sel_hi:[1,0,1] neg_lo:[0,0,1] neg_hi:[0,0,1]
	s_nop 0
	v_pk_mul_f32 v[70:71], v[56:57], v[10:11] op_sel:[1,0] op_sel_hi:[0,0] neg_lo:[1,1] neg_hi:[0,1]
	s_nop 0
	v_pk_fma_f32 v[56:57], v[56:57], v[10:11], v[70:71] op_sel_hi:[1,0,1]
	v_pk_fma_f32 v[70:71], v[64:65], v[50:51], v[96:97] op_sel_hi:[1,0,1]
	v_pk_fma_f32 v[50:51], v[64:65], v[50:51], v[96:97] op_sel_hi:[1,0,1] neg_lo:[0,0,1] neg_hi:[0,0,1]
	s_nop 0
	v_pk_mul_f32 v[64:65], v[50:51], v[122:123] op_sel_hi:[1,0]
	v_xor_b32_e32 v86, 0x80000000, v51
	v_mov_b32_e32 v87, v50
	v_pk_fma_f32 v[50:51], v[60:61], v[44:45], v[98:99] op_sel_hi:[1,0,1]
	v_pk_fma_f32 v[44:45], v[60:61], v[44:45], v[98:99] op_sel_hi:[1,0,1] neg_lo:[0,0,1] neg_hi:[0,0,1]
	v_pk_fma_f32 v[64:65], v[86:87], v[120:121], v[64:65] op_sel_hi:[1,0,1] neg_lo:[0,1,0] neg_hi:[0,1,0]
	v_pk_mul_f32 v[60:61], v[44:45], v[36:37] op_sel_hi:[1,0]
	v_xor_b32_e32 v86, 0x80000000, v45
	v_mov_b32_e32 v87, v44
	s_waitcnt vmcnt(2)
	v_pk_fma_f32 v[44:45], v[58:59], v[48:49], v[100:101] op_sel_hi:[1,0,1]
	v_pk_fma_f32 v[48:49], v[58:59], v[48:49], v[100:101] op_sel_hi:[1,0,1] neg_lo:[0,0,1] neg_hi:[0,0,1]
	v_pk_fma_f32 v[60:61], v[86:87], v[32:33], v[60:61] op_sel_hi:[1,0,1] neg_lo:[0,1,0] neg_hi:[0,1,0]
	v_pk_mul_f32 v[58:59], v[48:49], v[124:125] op_sel_hi:[1,0]
	s_nop 0
	v_pk_fma_f32 v[48:49], v[48:49], v[118:119], v[58:59] op_sel:[1,0,0] op_sel_hi:[0,0,1] neg_lo:[1,1,0] neg_hi:[0,1,0]
	v_pk_fma_f32 v[58:59], v[54:55], v[38:39], v[102:103] op_sel_hi:[1,0,1]
	v_pk_fma_f32 v[38:39], v[54:55], v[38:39], v[102:103] op_sel_hi:[1,0,1] neg_lo:[0,0,1] neg_hi:[0,0,1]
	s_nop 0
	v_xor_b32_e32 v55, 0x80000000, v38
	v_mov_b32_e32 v54, v39
	v_pk_fma_f32 v[38:39], v[52:53], v[30:31], v[104:105] op_sel_hi:[1,0,1]
	v_pk_fma_f32 v[30:31], v[52:53], v[30:31], v[104:105] op_sel_hi:[1,0,1] neg_lo:[0,0,1] neg_hi:[0,0,1]
	s_nop 0
	v_pk_mul_f32 v[52:53], v[30:31], v[124:125] op_sel_hi:[1,0] neg_lo:[0,1] neg_hi:[0,1]
	v_xor_b32_e32 v86, 0x80000000, v31
	v_mov_b32_e32 v87, v30
	v_pk_fma_f32 v[30:31], v[46:47], v[26:27], v[106:107] op_sel_hi:[1,0,1]
	v_pk_fma_f32 v[26:27], v[46:47], v[26:27], v[106:107] op_sel_hi:[1,0,1] neg_lo:[0,0,1] neg_hi:[0,0,1]
	v_pk_fma_f32 v[52:53], v[86:87], v[118:119], v[52:53] op_sel_hi:[1,0,1] neg_lo:[0,1,0] neg_hi:[0,1,0]
	v_pk_mul_f32 v[46:47], v[26:27], v[36:37] op_sel_hi:[1,0] neg_lo:[0,1] neg_hi:[0,1]
	v_xor_b32_e32 v86, 0x80000000, v27
	v_mov_b32_e32 v87, v26
	s_waitcnt vmcnt(1)
	v_pk_fma_f32 v[26:27], v[42:43], v[28:29], v[108:109] op_sel_hi:[1,0,1]
	v_pk_fma_f32 v[28:29], v[42:43], v[28:29], v[108:109] op_sel_hi:[1,0,1] neg_lo:[0,0,1] neg_hi:[0,0,1]
	v_pk_fma_f32 v[86:87], v[86:87], v[32:33], v[46:47] op_sel_hi:[1,0,1] neg_lo:[0,1,0] neg_hi:[0,1,0]
	v_pk_mul_f32 v[42:43], v[28:29], v[122:123] op_sel_hi:[1,0] neg_lo:[0,1] neg_hi:[0,1]
	v_xor_b32_e32 v46, 0x80000000, v29
	v_mov_b32_e32 v47, v28
	v_pk_fma_f32 v[28:29], v[40:41], v[24:25], v[110:111] op_sel_hi:[1,0,1]
	v_pk_fma_f32 v[24:25], v[40:41], v[24:25], v[110:111] op_sel_hi:[1,0,1] neg_lo:[0,0,1] neg_hi:[0,0,1]
	v_pk_fma_f32 v[42:43], v[46:47], v[120:121], v[42:43] op_sel_hi:[1,0,1] neg_lo:[0,1,0] neg_hi:[0,1,0]
	v_pk_mul_f32 v[40:41], v[24:25], v[10:11] op_sel:[1,0] op_sel_hi:[0,0] neg_lo:[1,1] neg_hi:[0,1]
	s_nop 0
	v_pk_fma_f32 v[88:89], v[24:25], v[10:11], v[40:41] op_sel_hi:[1,0,1] neg_lo:[0,1,0] neg_hi:[0,1,0]
	v_pk_fma_f32 v[24:25], v[34:35], v[22:23], v[112:113] op_sel_hi:[1,0,1]
	v_pk_fma_f32 v[22:23], v[34:35], v[22:23], v[112:113] op_sel_hi:[1,0,1] neg_lo:[0,0,1] neg_hi:[0,0,1]
	v_pk_add_f32 v[40:41], v[84:85], v[38:39]
	v_pk_mul_f32 v[34:35], v[22:23], v[122:123] op_sel:[1,0] op_sel_hi:[0,0] neg_lo:[1,1] neg_hi:[0,1]
	v_pk_add_f32 v[38:39], v[84:85], v[38:39] neg_lo:[0,1] neg_hi:[0,1]
	v_pk_fma_f32 v[90:91], v[22:23], v[120:121], v[34:35] op_sel_hi:[1,0,1] neg_lo:[0,1,0] neg_hi:[0,1,0]
	v_pk_fma_f32 v[22:23], v[66:67], v[20:21], v[114:115] op_sel_hi:[1,0,1]
	v_pk_fma_f32 v[20:21], v[66:67], v[20:21], v[114:115] op_sel_hi:[1,0,1] neg_lo:[0,0,1] neg_hi:[0,0,1]
	s_nop 0
	v_pk_mul_f32 v[34:35], v[20:21], v[36:37] op_sel:[1,0] op_sel_hi:[0,0] neg_lo:[1,1] neg_hi:[0,1]
	v_pk_fma_f32 v[66:67], v[20:21], v[32:33], v[34:35] op_sel_hi:[1,0,1] neg_lo:[0,1,0] neg_hi:[0,1,0]
	s_waitcnt vmcnt(0)
	v_pk_fma_f32 v[20:21], v[62:63], v[18:19], v[116:117] op_sel_hi:[1,0,1]
	v_pk_fma_f32 v[18:19], v[62:63], v[18:19], v[116:117] op_sel_hi:[1,0,1] neg_lo:[0,0,1] neg_hi:[0,0,1]
	v_pk_mul_f32 v[46:47], v[38:39], v[36:37] op_sel:[1,0] op_sel_hi:[0,0] neg_lo:[1,1] neg_hi:[0,1]
	v_pk_mul_f32 v[34:35], v[18:19], v[124:125] op_sel:[1,0] op_sel_hi:[0,0] neg_lo:[1,1] neg_hi:[0,1]
	v_pk_fma_f32 v[38:39], v[38:39], v[32:33], v[46:47] op_sel_hi:[1,0,1]
	v_pk_add_f32 v[46:47], v[82:83], v[30:31]
	v_pk_add_f32 v[30:31], v[82:83], v[30:31] neg_lo:[0,1] neg_hi:[0,1]
	v_pk_fma_f32 v[62:63], v[18:19], v[118:119], v[34:35] op_sel_hi:[1,0,1] neg_lo:[0,1,0] neg_hi:[0,1,0]
	v_pk_add_f32 v[18:19], v[126:127], v[58:59]
	v_pk_add_f32 v[34:35], v[126:127], v[58:59] neg_lo:[0,1] neg_hi:[0,1]
	v_pk_mul_f32 v[58:59], v[30:31], v[10:11] op_sel:[1,0] op_sel_hi:[0,0] neg_lo:[1,1] neg_hi:[0,1]
	s_nop 0
	v_pk_fma_f32 v[58:59], v[30:31], v[10:11], v[58:59] op_sel_hi:[1,0,1]
	v_pk_add_f32 v[30:31], v[80:81], v[26:27]
	v_pk_add_f32 v[26:27], v[80:81], v[26:27] neg_lo:[0,1] neg_hi:[0,1]
	s_nop 0
	v_pk_mul_f32 v[80:81], v[26:27], v[36:37] op_sel_hi:[1,0]
	v_xor_b32_e32 v82, 0x80000000, v27
	v_mov_b32_e32 v83, v26
	v_pk_add_f32 v[26:27], v[76:77], v[28:29]
	v_pk_add_f32 v[28:29], v[76:77], v[28:29] neg_lo:[0,1] neg_hi:[0,1]
	v_pk_fma_f32 v[80:81], v[82:83], v[32:33], v[80:81] op_sel_hi:[1,0,1] neg_lo:[0,1,0] neg_hi:[0,1,0]
	v_xor_b32_e32 v77, 0x80000000, v28
	v_mov_b32_e32 v76, v29
	v_pk_add_f32 v[28:29], v[70:71], v[24:25]
	v_pk_add_f32 v[24:25], v[70:71], v[24:25] neg_lo:[0,1] neg_hi:[0,1]
	s_nop 0
	v_pk_mul_f32 v[70:71], v[24:25], v[36:37] op_sel_hi:[1,0] neg_lo:[0,1] neg_hi:[0,1]
	s_nop 0
	v_pk_fma_f32 v[24:25], v[24:25], v[32:33], v[70:71] op_sel:[1,0,0] op_sel_hi:[0,0,1] neg_lo:[1,1,0] neg_hi:[0,1,0]
	v_pk_add_f32 v[70:71], v[50:51], v[22:23]
	v_pk_add_f32 v[22:23], v[50:51], v[22:23] neg_lo:[0,1] neg_hi:[0,1]
	s_nop 0
	v_pk_mul_f32 v[50:51], v[22:23], v[10:11] op_sel:[1,0] op_sel_hi:[0,0] neg_lo:[1,1] neg_hi:[0,1]
	s_nop 0
	v_pk_fma_f32 v[50:51], v[22:23], v[10:11], v[50:51] op_sel_hi:[1,0,1] neg_lo:[0,1,0] neg_hi:[0,1,0]
	v_pk_add_f32 v[22:23], v[44:45], v[20:21]
	v_pk_add_f32 v[20:21], v[44:45], v[20:21] neg_lo:[0,1] neg_hi:[0,1]
	s_nop 0
	v_pk_mul_f32 v[44:45], v[20:21], v[36:37] op_sel:[1,0] op_sel_hi:[0,0] neg_lo:[1,1] neg_hi:[0,1]
	s_nop 0
	v_pk_fma_f32 v[20:21], v[20:21], v[32:33], v[44:45] op_sel_hi:[1,0,1] neg_lo:[0,1,0] neg_hi:[0,1,0]
	v_pk_add_f32 v[44:45], v[18:19], v[26:27]
	v_pk_add_f32 v[18:19], v[18:19], v[26:27] neg_lo:[0,1] neg_hi:[0,1]
	v_pk_add_f32 v[26:27], v[40:41], v[28:29]
	v_pk_add_f32 v[28:29], v[40:41], v[28:29] neg_lo:[0,1] neg_hi:[0,1]
	s_nop 0
	v_pk_mul_f32 v[40:41], v[28:29], v[10:11] op_sel:[1,0] op_sel_hi:[0,0] neg_lo:[1,1] neg_hi:[0,1]
	s_nop 0
	v_pk_fma_f32 v[28:29], v[28:29], v[10:11], v[40:41] op_sel_hi:[1,0,1]
	v_pk_add_f32 v[40:41], v[46:47], v[70:71]
	v_pk_add_f32 v[46:47], v[46:47], v[70:71] neg_lo:[0,1] neg_hi:[0,1]
	s_nop 0
	v_xor_b32_e32 v71, 0x80000000, v46
	v_mov_b32_e32 v70, v47
	v_pk_add_f32 v[46:47], v[30:31], v[22:23]
	v_pk_add_f32 v[22:23], v[30:31], v[22:23] neg_lo:[0,1] neg_hi:[0,1]
	s_nop 0
	v_pk_mul_f32 v[30:31], v[22:23], v[10:11] op_sel:[1,0] op_sel_hi:[0,0] neg_lo:[1,1] neg_hi:[0,1]
	s_nop 0
	v_pk_fma_f32 v[82:83], v[22:23], v[10:11], v[30:31] op_sel_hi:[1,0,1] neg_lo:[0,1,0] neg_hi:[0,1,0]
	v_pk_add_f32 v[30:31], v[26:27], v[46:47]
	v_pk_add_f32 v[26:27], v[26:27], v[46:47] neg_lo:[0,1] neg_hi:[0,1]
	v_pk_add_f32 v[22:23], v[44:45], v[40:41]
	v_pk_add_f32 v[40:41], v[44:45], v[40:41] neg_lo:[0,1] neg_hi:[0,1]
	v_pk_add_f32 v[84:85], v[22:23], v[30:31]
	v_pk_add_f32 v[30:31], v[22:23], v[30:31] neg_lo:[0,1] neg_hi:[0,1]
	v_pk_add_f32 v[46:47], v[40:41], v[26:27] op_sel:[0,1] op_sel_hi:[1,0] neg_hi:[0,1]
	v_pk_add_f32 v[22:23], v[40:41], v[26:27] op_sel:[0,1] op_sel_hi:[1,0] neg_lo:[0,1]
	v_pk_add_f32 v[40:41], v[28:29], v[82:83]
	v_pk_add_f32 v[28:29], v[28:29], v[82:83] neg_lo:[0,1] neg_hi:[0,1]
	v_pk_add_f32 v[26:27], v[18:19], v[70:71]
	v_pk_add_f32 v[18:19], v[18:19], v[70:71] neg_lo:[0,1] neg_hi:[0,1]
	v_pk_add_f32 v[70:71], v[26:27], v[40:41]
	v_pk_add_f32 v[26:27], v[26:27], v[40:41] neg_lo:[0,1] neg_hi:[0,1]
	v_pk_add_f32 v[40:41], v[18:19], v[28:29] op_sel:[0,1] op_sel_hi:[1,0] neg_hi:[0,1]
	v_pk_add_f32 v[18:19], v[18:19], v[28:29] op_sel:[0,1] op_sel_hi:[1,0] neg_lo:[0,1]
	v_pk_add_f32 v[28:29], v[34:35], v[76:77]
	v_pk_add_f32 v[44:45], v[34:35], v[76:77] neg_lo:[0,1] neg_hi:[0,1]
	v_pk_add_f32 v[34:35], v[38:39], v[24:25]
	v_pk_add_f32 v[24:25], v[38:39], v[24:25] neg_lo:[0,1] neg_hi:[0,1]
	s_nop 0
	v_pk_mul_f32 v[38:39], v[10:11], v[24:25] op_sel:[0,1] op_sel_hi:[0,0] neg_lo:[1,1] neg_hi:[1,0]
	v_pk_fma_f32 v[38:39], v[10:11], v[24:25], v[38:39] op_sel_hi:[0,1,1]
	v_pk_add_f32 v[24:25], v[58:59], v[50:51]
	v_pk_add_f32 v[50:51], v[58:59], v[50:51] neg_lo:[0,1] neg_hi:[0,1]
	s_nop 0
	v_xor_b32_e32 v59, 0x80000000, v50
	v_mov_b32_e32 v58, v51
	v_pk_add_f32 v[50:51], v[80:81], v[20:21]
	v_pk_add_f32 v[20:21], v[80:81], v[20:21] neg_lo:[0,1] neg_hi:[0,1]
	s_nop 0
	v_pk_mul_f32 v[76:77], v[10:11], v[20:21] op_sel:[0,1] op_sel_hi:[0,0] neg_lo:[1,1] neg_hi:[1,0]
	v_pk_fma_f32 v[20:21], v[10:11], v[20:21], v[76:77] op_sel_hi:[0,1,1] neg_lo:[1,0,0] neg_hi:[1,0,0]
	v_pk_add_f32 v[76:77], v[28:29], v[24:25]
	v_pk_add_f32 v[24:25], v[28:29], v[24:25] neg_lo:[0,1] neg_hi:[0,1]
	v_pk_add_f32 v[28:29], v[34:35], v[50:51]
	v_pk_add_f32 v[34:35], v[34:35], v[50:51] neg_lo:[0,1] neg_hi:[0,1]
	v_pk_add_f32 v[82:83], v[76:77], v[28:29]
	v_xor_b32_e32 v81, 0x80000000, v34
	v_mov_b32_e32 v80, v35
	v_pk_add_f32 v[34:35], v[76:77], v[28:29] neg_lo:[0,1] neg_hi:[0,1]
	v_pk_add_f32 v[28:29], v[44:45], v[58:59]
	v_pk_add_f32 v[58:59], v[44:45], v[58:59] neg_lo:[0,1] neg_hi:[0,1]
	v_pk_add_f32 v[44:45], v[38:39], v[20:21]
	v_pk_add_f32 v[20:21], v[38:39], v[20:21] neg_lo:[0,1] neg_hi:[0,1]
	v_pk_add_f32 v[76:77], v[28:29], v[44:45]
	v_pk_add_f32 v[28:29], v[28:29], v[44:45] neg_lo:[0,1] neg_hi:[0,1]
	v_pk_add_f32 v[44:45], v[58:59], v[20:21] op_sel:[0,1] op_sel_hi:[1,0] neg_hi:[0,1]
	v_pk_add_f32 v[20:21], v[58:59], v[20:21] op_sel:[0,1] op_sel_hi:[1,0] neg_lo:[0,1]
	v_pk_add_f32 v[38:39], v[74:75], v[54:55]
	v_pk_add_f32 v[58:59], v[74:75], v[54:55] neg_lo:[0,1] neg_hi:[0,1]
	v_pk_add_f32 v[54:55], v[78:79], v[52:53]
	v_pk_add_f32 v[52:53], v[78:79], v[52:53] neg_lo:[0,1] neg_hi:[0,1]
	v_pk_add_f32 v[50:51], v[24:25], v[80:81]
	v_pk_mul_f32 v[74:75], v[36:37], v[52:53] op_sel:[0,1] op_sel_hi:[0,0] neg_lo:[1,1] neg_hi:[1,0]
	v_pk_fma_f32 v[52:53], v[32:33], v[52:53], v[74:75] op_sel_hi:[0,1,1]
	v_pk_add_f32 v[74:75], v[72:73], v[86:87]
	v_pk_add_f32 v[72:73], v[72:73], v[86:87] neg_lo:[0,1] neg_hi:[0,1]
	v_pk_add_f32 v[24:25], v[24:25], v[80:81] neg_lo:[0,1] neg_hi:[0,1]
	v_pk_mul_f32 v[78:79], v[10:11], v[72:73] op_sel:[0,1] op_sel_hi:[0,0] neg_lo:[1,1] neg_hi:[1,0]
	v_pk_fma_f32 v[72:73], v[10:11], v[72:73], v[78:79] op_sel_hi:[0,1,1]
	v_pk_add_f32 v[78:79], v[68:69], v[42:43]
	v_pk_add_f32 v[42:43], v[68:69], v[42:43] neg_lo:[0,1] neg_hi:[0,1]
	s_nop 0
	v_pk_mul_f32 v[68:69], v[32:33], v[42:43] op_sel:[0,1] op_sel_hi:[0,0] neg_lo:[1,1] neg_hi:[1,0]
	v_pk_fma_f32 v[42:43], v[36:37], v[42:43], v[68:69] op_sel_hi:[0,1,1]
	v_pk_add_f32 v[68:69], v[56:57], v[88:89]
	v_pk_add_f32 v[56:57], v[56:57], v[88:89] neg_lo:[0,1] neg_hi:[0,1]
	s_nop 0
	v_xor_b32_e32 v81, 0x80000000, v56
	v_mov_b32_e32 v80, v57
	v_pk_add_f32 v[56:57], v[64:65], v[90:91]
	v_pk_add_f32 v[64:65], v[64:65], v[90:91] neg_lo:[0,1] neg_hi:[0,1]
	s_nop 0
	v_pk_mul_f32 v[86:87], v[32:33], v[64:65] op_sel:[0,1] op_sel_hi:[0,0] neg_lo:[1,1] neg_hi:[1,0]
	v_pk_fma_f32 v[64:65], v[36:37], v[64:65], v[86:87] op_sel_hi:[0,1,1] neg_lo:[1,0,0] neg_hi:[1,0,0]
	v_pk_add_f32 v[86:87], v[60:61], v[66:67]
	v_pk_add_f32 v[60:61], v[60:61], v[66:67] neg_lo:[0,1] neg_hi:[0,1]
	s_nop 0
	v_pk_mul_f32 v[66:67], v[10:11], v[60:61] op_sel:[0,1] op_sel_hi:[0,0] neg_lo:[1,1] neg_hi:[1,0]
	v_pk_fma_f32 v[60:61], v[10:11], v[60:61], v[66:67] op_sel_hi:[0,1,1] neg_lo:[1,0,0] neg_hi:[1,0,0]
	v_pk_add_f32 v[66:67], v[48:49], v[62:63]
	v_pk_add_f32 v[48:49], v[48:49], v[62:63] neg_lo:[0,1] neg_hi:[0,1]
	s_nop 0
	v_pk_mul_f32 v[36:37], v[36:37], v[48:49] op_sel:[0,1] op_sel_hi:[0,0] neg_lo:[1,1] neg_hi:[1,0]
	v_pk_fma_f32 v[36:37], v[32:33], v[48:49], v[36:37] op_sel_hi:[0,1,1] neg_lo:[1,0,0] neg_hi:[1,0,0]
	v_pk_add_f32 v[32:33], v[38:39], v[68:69]
	v_pk_add_f32 v[48:49], v[38:39], v[68:69] neg_lo:[0,1] neg_hi:[0,1]
	v_pk_add_f32 v[38:39], v[56:57], v[54:55]
	v_pk_add_f32 v[54:55], v[54:55], v[56:57] neg_lo:[0,1] neg_hi:[0,1]
	v_pk_add_f32 v[62:63], v[74:75], v[86:87] neg_lo:[0,1] neg_hi:[0,1]
	v_pk_mul_f32 v[56:57], v[10:11], v[54:55] op_sel:[0,1] op_sel_hi:[0,0] neg_lo:[1,1] neg_hi:[1,0]
	v_xor_b32_e32 v69, 0x80000000, v62
	v_mov_b32_e32 v68, v63
	v_pk_add_f32 v[62:63], v[78:79], v[66:67]
	v_pk_add_f32 v[66:67], v[78:79], v[66:67] neg_lo:[0,1] neg_hi:[0,1]
	v_pk_fma_f32 v[56:57], v[10:11], v[54:55], v[56:57] op_sel_hi:[0,1,1]
	v_pk_add_f32 v[54:55], v[74:75], v[86:87]
	v_pk_mul_f32 v[74:75], v[10:11], v[66:67] op_sel:[0,1] op_sel_hi:[0,0] neg_lo:[1,1] neg_hi:[1,0]
	v_pk_fma_f32 v[66:67], v[10:11], v[66:67], v[74:75] op_sel_hi:[0,1,1] neg_lo:[1,0,0] neg_hi:[1,0,0]
	v_pk_add_f32 v[74:75], v[32:33], v[54:55]
	v_pk_add_f32 v[32:33], v[32:33], v[54:55] neg_lo:[0,1] neg_hi:[0,1]
	v_pk_add_f32 v[54:55], v[38:39], v[62:63]
	v_pk_add_f32 v[38:39], v[38:39], v[62:63] neg_lo:[0,1] neg_hi:[0,1]
	v_pk_add_f32 v[78:79], v[74:75], v[54:55]
	v_pk_add_f32 v[54:55], v[74:75], v[54:55] neg_lo:[0,1] neg_hi:[0,1]
	v_pk_add_f32 v[74:75], v[32:33], v[38:39] op_sel:[0,1] op_sel_hi:[1,0] neg_hi:[0,1]
	v_pk_add_f32 v[38:39], v[32:33], v[38:39] op_sel:[0,1] op_sel_hi:[1,0] neg_lo:[0,1]
	v_pk_add_f32 v[32:33], v[48:49], v[68:69]
	v_pk_add_f32 v[62:63], v[48:49], v[68:69] neg_lo:[0,1] neg_hi:[0,1]
	v_pk_add_f32 v[48:49], v[56:57], v[66:67]
	v_pk_add_f32 v[56:57], v[56:57], v[66:67] neg_lo:[0,1] neg_hi:[0,1]
	s_nop 0
	v_xor_b32_e32 v67, 0x80000000, v56
	v_mov_b32_e32 v66, v57
	v_pk_add_f32 v[56:57], v[32:33], v[48:49]
	v_pk_add_f32 v[48:49], v[32:33], v[48:49] neg_lo:[0,1] neg_hi:[0,1]
	v_pk_add_f32 v[68:69], v[62:63], v[66:67]
	v_pk_add_f32 v[32:33], v[62:63], v[66:67] neg_lo:[0,1] neg_hi:[0,1]
	v_pk_add_f32 v[66:67], v[64:65], v[52:53]
	v_pk_add_f32 v[52:53], v[52:53], v[64:65] neg_lo:[0,1] neg_hi:[0,1]
	v_pk_add_f32 v[62:63], v[58:59], v[80:81]
	v_pk_mul_f32 v[64:65], v[10:11], v[52:53] op_sel:[0,1] op_sel_hi:[0,0] neg_lo:[1,1] neg_hi:[1,0]
	v_pk_fma_f32 v[52:53], v[10:11], v[52:53], v[64:65] op_sel_hi:[0,1,1]
	v_pk_add_f32 v[64:65], v[72:73], v[60:61]
	v_pk_add_f32 v[60:61], v[72:73], v[60:61] neg_lo:[0,1] neg_hi:[0,1]
	v_pk_add_f32 v[58:59], v[58:59], v[80:81] neg_lo:[0,1] neg_hi:[0,1]
	v_xor_b32_e32 v73, 0x80000000, v60
	v_mov_b32_e32 v72, v61
	v_pk_add_f32 v[60:61], v[42:43], v[36:37]
	v_pk_add_f32 v[36:37], v[42:43], v[36:37] neg_lo:[0,1] neg_hi:[0,1]
	s_nop 0
	v_pk_mul_f32 v[42:43], v[10:11], v[36:37] op_sel:[0,1] op_sel_hi:[0,0] neg_lo:[1,1] neg_hi:[1,0]
	v_pk_fma_f32 v[36:37], v[10:11], v[36:37], v[42:43] op_sel_hi:[0,1,1] neg_lo:[1,0,0] neg_hi:[1,0,0]
	v_pk_add_f32 v[42:43], v[62:63], v[64:65]
	v_pk_add_f32 v[62:63], v[62:63], v[64:65] neg_lo:[0,1] neg_hi:[0,1]
	v_pk_add_f32 v[64:65], v[66:67], v[60:61]
	v_pk_add_f32 v[60:61], v[66:67], v[60:61] neg_lo:[0,1] neg_hi:[0,1]
	v_lshl_add_u32 v10, v13, 3, 0
	v_xor_b32_e32 v67, 0x80000000, v60
	v_mov_b32_e32 v66, v61
	v_pk_add_f32 v[60:61], v[42:43], v[64:65]
	v_pk_add_f32 v[64:65], v[42:43], v[64:65] neg_lo:[0,1] neg_hi:[0,1]
	v_pk_add_f32 v[80:81], v[62:63], v[66:67]
	v_pk_add_f32 v[42:43], v[62:63], v[66:67] neg_lo:[0,1] neg_hi:[0,1]
	v_pk_add_f32 v[66:67], v[52:53], v[36:37]
	v_pk_add_f32 v[36:37], v[52:53], v[36:37] neg_lo:[0,1] neg_hi:[0,1]
	v_pk_add_f32 v[62:63], v[58:59], v[72:73]
	v_pk_add_f32 v[58:59], v[58:59], v[72:73] neg_lo:[0,1] neg_hi:[0,1]
	v_pk_add_f32 v[86:87], v[62:63], v[66:67]
	v_pk_add_f32 v[52:53], v[62:63], v[66:67] neg_lo:[0,1] neg_hi:[0,1]
	v_pk_add_f32 v[62:63], v[58:59], v[36:37] op_sel:[0,1] op_sel_hi:[1,0] neg_hi:[0,1]
	v_pk_add_f32 v[36:37], v[58:59], v[36:37] op_sel:[0,1] op_sel_hi:[1,0] neg_lo:[0,1]
	v_pk_mul_f32 v[58:59], v[84:85], s[14:15] op_sel:[1,0] neg_lo:[1,0]
	s_nop 0
	v_pk_fma_f32 v[58:59], v[84:85], s[94:95], v[58:59] op_sel_hi:[0,1,1]
	ds_write_b64 v10, v[58:59]
	v_pk_fma_f32 v[58:59], v[178:179], s[90:91], v[178:179] op_sel:[1,0,0] op_sel_hi:[0,1,1]
	v_pk_mul_f32 v[66:67], v[58:59], v[78:79] op_sel:[1,1] op_sel_hi:[0,1] neg_lo:[0,1]
	v_pk_fma_f32 v[66:67], v[58:59], v[78:79], v[66:67] op_sel_hi:[1,0,1]
	ds_write_b64 v10, v[66:67] offset:4224
	v_pk_mul_f32 v[66:67], v[178:179], v[58:59] op_sel:[1,1] op_sel_hi:[0,1] neg_lo:[0,1]
	v_pk_fma_f32 v[58:59], v[178:179], v[58:59], v[66:67] op_sel_hi:[1,0,1]
	s_nop 0
	v_pk_mul_f32 v[66:67], v[58:59], v[82:83] op_sel:[1,1] op_sel_hi:[0,1] neg_lo:[0,1]
	v_pk_fma_f32 v[66:67], v[58:59], v[82:83], v[66:67] op_sel_hi:[1,0,1]
	ds_write_b64 v10, v[66:67] offset:8448
	v_pk_mul_f32 v[66:67], v[178:179], v[58:59] op_sel:[1,1] op_sel_hi:[0,1] neg_lo:[0,1]
	v_pk_fma_f32 v[58:59], v[178:179], v[58:59], v[66:67] op_sel_hi:[1,0,1]
	s_nop 0
	v_pk_mul_f32 v[66:67], v[58:59], v[60:61] op_sel:[1,1] op_sel_hi:[0,1] neg_lo:[0,1]
	v_pk_fma_f32 v[60:61], v[58:59], v[60:61], v[66:67] op_sel_hi:[1,0,1]
	ds_write_b64 v10, v[60:61] offset:12672
	v_pk_mul_f32 v[60:61], v[178:179], v[58:59] op_sel:[1,1] op_sel_hi:[0,1] neg_lo:[0,1]
	v_pk_fma_f32 v[58:59], v[178:179], v[58:59], v[60:61] op_sel_hi:[1,0,1]
	s_nop 0
	v_pk_mul_f32 v[60:61], v[70:71], v[58:59] op_sel:[1,1] op_sel_hi:[1,0] neg_lo:[1,0]
	s_nop 0
	v_pk_fma_f32 v[60:61], v[70:71], v[58:59], v[60:61] op_sel_hi:[0,1,1]
	ds_write_b64 v10, v[60:61] offset:16896
	v_pk_mul_f32 v[60:61], v[178:179], v[58:59] op_sel:[1,1] op_sel_hi:[0,1] neg_lo:[0,1]
	v_pk_fma_f32 v[58:59], v[178:179], v[58:59], v[60:61] op_sel_hi:[1,0,1]
	s_nop 0
	v_pk_mul_f32 v[60:61], v[58:59], v[56:57] op_sel:[1,1] op_sel_hi:[0,1] neg_lo:[0,1]
	v_pk_fma_f32 v[56:57], v[58:59], v[56:57], v[60:61] op_sel_hi:[1,0,1]
	ds_write_b64 v10, v[56:57] offset:21120
	v_pk_mul_f32 v[56:57], v[178:179], v[58:59] op_sel:[1,1] op_sel_hi:[0,1] neg_lo:[0,1]
	v_pk_fma_f32 v[56:57], v[178:179], v[58:59], v[56:57] op_sel_hi:[1,0,1]
	s_nop 0
	v_pk_mul_f32 v[58:59], v[76:77], v[56:57] op_sel:[1,1] op_sel_hi:[1,0] neg_lo:[1,0]
	s_nop 0
	v_pk_fma_f32 v[58:59], v[76:77], v[56:57], v[58:59] op_sel_hi:[0,1,1]
	ds_write_b64 v10, v[58:59] offset:25344
	v_pk_mul_f32 v[58:59], v[178:179], v[56:57] op_sel:[1,1] op_sel_hi:[0,1] neg_lo:[0,1]
	v_pk_fma_f32 v[56:57], v[178:179], v[56:57], v[58:59] op_sel_hi:[1,0,1]
	s_nop 0
	v_pk_mul_f32 v[58:59], v[86:87], v[56:57] op_sel:[1,1] op_sel_hi:[1,0] neg_lo:[1,0]
	s_nop 0
	v_pk_fma_f32 v[58:59], v[86:87], v[56:57], v[58:59] op_sel_hi:[0,1,1]
	ds_write_b64 v10, v[58:59] offset:29568
	v_pk_mul_f32 v[58:59], v[178:179], v[56:57] op_sel:[1,1] op_sel_hi:[0,1] neg_lo:[0,1]
	v_pk_fma_f32 v[56:57], v[178:179], v[56:57], v[58:59] op_sel_hi:[1,0,1]
	s_nop 0
	v_pk_mul_f32 v[58:59], v[46:47], v[56:57] op_sel:[1,1] op_sel_hi:[1,0] neg_lo:[1,0]
	s_nop 0
	v_pk_fma_f32 v[46:47], v[46:47], v[56:57], v[58:59] op_sel_hi:[0,1,1]
	ds_write_b64 v10, v[46:47] offset:33792
	v_pk_mul_f32 v[46:47], v[178:179], v[56:57] op_sel:[1,1] op_sel_hi:[0,1] neg_lo:[0,1]
	v_pk_fma_f32 v[46:47], v[178:179], v[56:57], v[46:47] op_sel_hi:[1,0,1]
	s_nop 0
	v_pk_mul_f32 v[56:57], v[74:75], v[46:47] op_sel:[1,1] op_sel_hi:[1,0] neg_lo:[1,0]
	s_nop 0
	v_pk_fma_f32 v[56:57], v[74:75], v[46:47], v[56:57] op_sel_hi:[0,1,1]
	ds_write_b64 v10, v[56:57] offset:38016
	v_pk_mul_f32 v[56:57], v[178:179], v[46:47] op_sel:[1,1] op_sel_hi:[0,1] neg_lo:[0,1]
	v_pk_fma_f32 v[46:47], v[178:179], v[46:47], v[56:57] op_sel_hi:[1,0,1]
	s_nop 0
	v_pk_mul_f32 v[56:57], v[50:51], v[46:47] op_sel:[1,1] op_sel_hi:[1,0] neg_lo:[1,0]
	s_nop 0
	v_pk_fma_f32 v[50:51], v[50:51], v[46:47], v[56:57] op_sel_hi:[0,1,1]
	ds_write_b64 v10, v[50:51] offset:42240
	v_pk_mul_f32 v[50:51], v[178:179], v[46:47] op_sel:[1,1] op_sel_hi:[0,1] neg_lo:[0,1]
	v_pk_fma_f32 v[46:47], v[178:179], v[46:47], v[50:51] op_sel_hi:[1,0,1]
	s_nop 0
	v_pk_mul_f32 v[50:51], v[80:81], v[46:47] op_sel:[1,1] op_sel_hi:[1,0] neg_lo:[1,0]
	s_nop 0
	v_pk_fma_f32 v[50:51], v[80:81], v[46:47], v[50:51] op_sel_hi:[0,1,1]
	ds_write_b64 v10, v[50:51] offset:46464
	v_pk_mul_f32 v[50:51], v[178:179], v[46:47] op_sel:[1,1] op_sel_hi:[0,1] neg_lo:[0,1]
	v_pk_fma_f32 v[46:47], v[178:179], v[46:47], v[50:51] op_sel_hi:[1,0,1]
	s_nop 0
	v_pk_mul_f32 v[50:51], v[40:41], v[46:47] op_sel:[1,1] op_sel_hi:[1,0] neg_lo:[1,0]
	s_nop 0
	v_pk_fma_f32 v[40:41], v[40:41], v[46:47], v[50:51] op_sel_hi:[0,1,1]
	ds_write_b64 v10, v[40:41] offset:50688
	v_pk_mul_f32 v[40:41], v[178:179], v[46:47] op_sel:[1,1] op_sel_hi:[0,1] neg_lo:[0,1]
	v_pk_fma_f32 v[40:41], v[178:179], v[46:47], v[40:41] op_sel_hi:[1,0,1]
	s_nop 0
	v_pk_mul_f32 v[46:47], v[68:69], v[40:41] op_sel:[1,1] op_sel_hi:[1,0] neg_lo:[1,0]
	s_nop 0
	v_pk_fma_f32 v[46:47], v[68:69], v[40:41], v[46:47] op_sel_hi:[0,1,1]
	ds_write_b64 v10, v[46:47] offset:54912
	v_pk_mul_f32 v[46:47], v[178:179], v[40:41] op_sel:[1,1] op_sel_hi:[0,1] neg_lo:[0,1]
	v_pk_fma_f32 v[40:41], v[178:179], v[40:41], v[46:47] op_sel_hi:[1,0,1]
	s_nop 0
	v_pk_mul_f32 v[46:47], v[44:45], v[40:41] op_sel:[1,1] op_sel_hi:[1,0] neg_lo:[1,0]
	s_nop 0
	v_pk_fma_f32 v[44:45], v[44:45], v[40:41], v[46:47] op_sel_hi:[0,1,1]
	ds_write_b64 v10, v[44:45] offset:59136
	v_pk_mul_f32 v[44:45], v[178:179], v[40:41] op_sel:[1,1] op_sel_hi:[0,1] neg_lo:[0,1]
	v_pk_fma_f32 v[40:41], v[178:179], v[40:41], v[44:45] op_sel_hi:[1,0,1]
	s_nop 0
	v_pk_mul_f32 v[44:45], v[62:63], v[40:41] op_sel:[1,1] op_sel_hi:[1,0] neg_lo:[1,0]
	s_nop 0
	v_pk_fma_f32 v[44:45], v[62:63], v[40:41], v[44:45] op_sel_hi:[0,1,1]
	ds_write_b64 v10, v[44:45] offset:63360
	v_pk_mul_f32 v[44:45], v[178:179], v[40:41] op_sel:[1,1] op_sel_hi:[0,1] neg_lo:[0,1]
	v_pk_fma_f32 v[40:41], v[178:179], v[40:41], v[44:45] op_sel_hi:[1,0,1]
	s_nop 0
	v_pk_mul_f32 v[44:45], v[30:31], v[40:41] op_sel:[1,1] op_sel_hi:[1,0] neg_lo:[1,0]
	v_add_u32_e32 v13, 0x10800, v10
	v_pk_fma_f32 v[30:31], v[30:31], v[40:41], v[44:45] op_sel_hi:[0,1,1]
	ds_write_b64 v13, v[30:31]
	v_pk_mul_f32 v[30:31], v[178:179], v[40:41] op_sel:[1,1] op_sel_hi:[0,1] neg_lo:[0,1]
	v_pk_fma_f32 v[30:31], v[178:179], v[40:41], v[30:31] op_sel_hi:[1,0,1]
	s_nop 0
	v_pk_mul_f32 v[40:41], v[54:55], v[30:31] op_sel:[1,1] op_sel_hi:[1,0] neg_lo:[1,0]
	v_add_u32_e32 v13, 0x11880, v10
	v_pk_fma_f32 v[40:41], v[54:55], v[30:31], v[40:41] op_sel_hi:[0,1,1]
	ds_write_b64 v13, v[40:41]
	v_pk_mul_f32 v[40:41], v[178:179], v[30:31] op_sel:[1,1] op_sel_hi:[0,1] neg_lo:[0,1]
	v_pk_fma_f32 v[30:31], v[178:179], v[30:31], v[40:41] op_sel_hi:[1,0,1]
	s_nop 0
	v_pk_mul_f32 v[40:41], v[34:35], v[30:31] op_sel:[1,1] op_sel_hi:[1,0] neg_lo:[1,0]
	v_add_u32_e32 v13, 0x12900, v10
	v_pk_fma_f32 v[34:35], v[34:35], v[30:31], v[40:41] op_sel_hi:[0,1,1]
	ds_write_b64 v13, v[34:35]
	v_pk_mul_f32 v[34:35], v[178:179], v[30:31] op_sel:[1,1] op_sel_hi:[0,1] neg_lo:[0,1]
	v_pk_fma_f32 v[30:31], v[178:179], v[30:31], v[34:35] op_sel_hi:[1,0,1]
	s_nop 0
	v_pk_mul_f32 v[34:35], v[64:65], v[30:31] op_sel:[1,1] op_sel_hi:[1,0] neg_lo:[1,0]
	v_add_u32_e32 v13, 0x13980, v10
	v_pk_fma_f32 v[34:35], v[64:65], v[30:31], v[34:35] op_sel_hi:[0,1,1]
	ds_write_b64 v13, v[34:35]
	v_pk_mul_f32 v[34:35], v[178:179], v[30:31] op_sel:[1,1] op_sel_hi:[0,1] neg_lo:[0,1]
	v_pk_fma_f32 v[30:31], v[178:179], v[30:31], v[34:35] op_sel_hi:[1,0,1]
	s_nop 0
	v_pk_mul_f32 v[34:35], v[26:27], v[30:31] op_sel:[1,1] op_sel_hi:[1,0] neg_lo:[1,0]
	v_add_u32_e32 v13, 0x14a00, v10
	v_pk_fma_f32 v[26:27], v[26:27], v[30:31], v[34:35] op_sel_hi:[0,1,1]
	ds_write_b64 v13, v[26:27]
	v_pk_mul_f32 v[26:27], v[178:179], v[30:31] op_sel:[1,1] op_sel_hi:[0,1] neg_lo:[0,1]
	v_pk_fma_f32 v[26:27], v[178:179], v[30:31], v[26:27] op_sel_hi:[1,0,1]
	s_nop 0
	v_pk_mul_f32 v[30:31], v[48:49], v[26:27] op_sel:[1,1] op_sel_hi:[1,0] neg_lo:[1,0]
	v_add_u32_e32 v13, 0x15a80, v10
	v_pk_fma_f32 v[30:31], v[48:49], v[26:27], v[30:31] op_sel_hi:[0,1,1]
	ds_write_b64 v13, v[30:31]
	v_pk_mul_f32 v[30:31], v[178:179], v[26:27] op_sel:[1,1] op_sel_hi:[0,1] neg_lo:[0,1]
	v_pk_fma_f32 v[26:27], v[178:179], v[26:27], v[30:31] op_sel_hi:[1,0,1]
	s_nop 0
	v_pk_mul_f32 v[30:31], v[28:29], v[26:27] op_sel:[1,1] op_sel_hi:[1,0] neg_lo:[1,0]
	v_add_u32_e32 v13, 0x16b00, v10
	v_pk_fma_f32 v[28:29], v[28:29], v[26:27], v[30:31] op_sel_hi:[0,1,1]
	ds_write_b64 v13, v[28:29]
	v_pk_mul_f32 v[28:29], v[178:179], v[26:27] op_sel:[1,1] op_sel_hi:[0,1] neg_lo:[0,1]
	v_pk_fma_f32 v[26:27], v[178:179], v[26:27], v[28:29] op_sel_hi:[1,0,1]
	s_nop 0
	v_pk_mul_f32 v[28:29], v[52:53], v[26:27] op_sel:[1,1] op_sel_hi:[1,0] neg_lo:[1,0]
	v_add_u32_e32 v13, 0x17b80, v10
	v_pk_fma_f32 v[28:29], v[52:53], v[26:27], v[28:29] op_sel_hi:[0,1,1]
	ds_write_b64 v13, v[28:29]
	v_pk_mul_f32 v[28:29], v[178:179], v[26:27] op_sel:[1,1] op_sel_hi:[0,1] neg_lo:[0,1]
	v_pk_fma_f32 v[26:27], v[178:179], v[26:27], v[28:29] op_sel_hi:[1,0,1]
	s_nop 0
	v_pk_mul_f32 v[28:29], v[22:23], v[26:27] op_sel:[1,1] op_sel_hi:[1,0] neg_lo:[1,0]
	v_add_u32_e32 v13, 0x18c00, v10
	v_pk_fma_f32 v[22:23], v[22:23], v[26:27], v[28:29] op_sel_hi:[0,1,1]
	ds_write_b64 v13, v[22:23]
	v_pk_mul_f32 v[22:23], v[178:179], v[26:27] op_sel:[1,1] op_sel_hi:[0,1] neg_lo:[0,1]
	v_pk_fma_f32 v[22:23], v[178:179], v[26:27], v[22:23] op_sel_hi:[1,0,1]
	s_nop 0
	v_pk_mul_f32 v[26:27], v[38:39], v[22:23] op_sel:[1,1] op_sel_hi:[1,0] neg_lo:[1,0]
	v_add_u32_e32 v13, 0x19c80, v10
	v_pk_fma_f32 v[26:27], v[38:39], v[22:23], v[26:27] op_sel_hi:[0,1,1]
	ds_write_b64 v13, v[26:27]
	v_pk_mul_f32 v[26:27], v[178:179], v[22:23] op_sel:[1,1] op_sel_hi:[0,1] neg_lo:[0,1]
	v_pk_fma_f32 v[22:23], v[178:179], v[22:23], v[26:27] op_sel_hi:[1,0,1]
	s_nop 0
	v_pk_mul_f32 v[26:27], v[24:25], v[22:23] op_sel:[1,1] op_sel_hi:[1,0] neg_lo:[1,0]
	v_add_u32_e32 v13, 0x1ad00, v10
	v_pk_fma_f32 v[24:25], v[24:25], v[22:23], v[26:27] op_sel_hi:[0,1,1]
	ds_write_b64 v13, v[24:25]
	v_pk_mul_f32 v[24:25], v[178:179], v[22:23] op_sel:[1,1] op_sel_hi:[0,1] neg_lo:[0,1]
	v_pk_fma_f32 v[22:23], v[178:179], v[22:23], v[24:25] op_sel_hi:[1,0,1]
	s_nop 0
	v_pk_mul_f32 v[24:25], v[42:43], v[22:23] op_sel:[1,1] op_sel_hi:[1,0] neg_lo:[1,0]
	v_add_u32_e32 v13, 0x1bd80, v10
	v_pk_fma_f32 v[24:25], v[42:43], v[22:23], v[24:25] op_sel_hi:[0,1,1]
	ds_write_b64 v13, v[24:25]
	v_pk_mul_f32 v[24:25], v[178:179], v[22:23] op_sel:[1,1] op_sel_hi:[0,1] neg_lo:[0,1]
	v_pk_fma_f32 v[22:23], v[178:179], v[22:23], v[24:25] op_sel_hi:[1,0,1]
	s_nop 0
	v_pk_mul_f32 v[24:25], v[18:19], v[22:23] op_sel:[1,1] op_sel_hi:[1,0] neg_lo:[1,0]
	v_add_u32_e32 v13, 0x1ce00, v10
	v_pk_fma_f32 v[18:19], v[18:19], v[22:23], v[24:25] op_sel_hi:[0,1,1]
	ds_write_b64 v13, v[18:19]
	v_pk_mul_f32 v[18:19], v[178:179], v[22:23] op_sel:[1,1] op_sel_hi:[0,1] neg_lo:[0,1]
	v_pk_fma_f32 v[18:19], v[178:179], v[22:23], v[18:19] op_sel_hi:[1,0,1]
	s_nop 0
	v_pk_mul_f32 v[22:23], v[32:33], v[18:19] op_sel:[1,1] op_sel_hi:[1,0] neg_lo:[1,0]
	v_add_u32_e32 v13, 0x1de80, v10
	v_pk_fma_f32 v[22:23], v[32:33], v[18:19], v[22:23] op_sel_hi:[0,1,1]
	ds_write_b64 v13, v[22:23]
	v_pk_mul_f32 v[22:23], v[178:179], v[18:19] op_sel:[1,1] op_sel_hi:[0,1] neg_lo:[0,1]
	v_pk_fma_f32 v[18:19], v[178:179], v[18:19], v[22:23] op_sel_hi:[1,0,1]
	s_nop 0
	v_pk_mul_f32 v[22:23], v[20:21], v[18:19] op_sel:[1,1] op_sel_hi:[1,0] neg_lo:[1,0]
	v_add_u32_e32 v13, 0x1ef00, v10
	v_pk_fma_f32 v[20:21], v[20:21], v[18:19], v[22:23] op_sel_hi:[0,1,1]
	ds_write_b64 v13, v[20:21]
	v_pk_mul_f32 v[20:21], v[178:179], v[18:19] op_sel:[1,1] op_sel_hi:[0,1] neg_lo:[0,1]
	v_pk_fma_f32 v[16:17], v[178:179], v[18:19], v[20:21] op_sel_hi:[1,0,1]
	s_nop 0
	v_pk_mul_f32 v[18:19], v[36:37], v[16:17] op_sel:[1,1] op_sel_hi:[1,0] neg_lo:[1,0]
	v_add_u32_e32 v10, 0x1ff80, v10
	v_pk_fma_f32 v[16:17], v[36:37], v[16:17], v[18:19] op_sel_hi:[0,1,1]
	ds_write_b64 v10, v[16:17]
	v_mov_b32_e32 v10, v174
	v_mov_b32_e32 v13, v172
	s_waitcnt lgkmcnt(0)
	s_barrier
	v_mov_b32_e32 v16, v180
	v_add_u32_e32 v15, v13, v10
	v_lshl_add_u32 v75, v15, 3, 0
	v_xad_u32 v15, v13, 1, v10
	v_lshl_add_u32 v74, v15, 3, 0
	v_xad_u32 v15, v13, 2, v10
	v_lshl_add_u32 v73, v15, 3, 0
	v_xad_u32 v15, v13, 3, v10
	v_lshl_add_u32 v72, v15, 3, 0
	v_xad_u32 v15, v13, 4, v10
	v_lshl_add_u32 v71, v15, 3, 0
	v_xad_u32 v15, v13, 5, v10
	v_lshl_add_u32 v70, v15, 3, 0
	v_xad_u32 v15, v13, 6, v10
	v_lshl_add_u32 v69, v15, 3, 0
	v_xad_u32 v15, v13, 7, v10
	v_lshl_add_u32 v68, v15, 3, 0
	v_xad_u32 v15, v13, 8, v10
	v_lshl_add_u32 v15, v15, 3, 0
	v_add_u32_e32 v67, 0x800, v15
	v_xad_u32 v15, v13, 9, v10
	v_lshl_add_u32 v15, v15, 3, 0
	v_add_u32_e32 v66, 0x800, v15
	v_xad_u32 v15, v13, 10, v10
	v_lshl_add_u32 v15, v15, 3, 0
	v_add_u32_e32 v65, 0x800, v15
	v_xad_u32 v15, v13, 11, v10
	v_lshl_add_u32 v15, v15, 3, 0
	v_add_u32_e32 v64, 0x800, v15
	v_xad_u32 v15, v13, 12, v10
	v_mov_b32_e32 v17, v181
	v_lshl_add_u32 v15, v15, 3, 0
	ds_read2_b64 v[18:21], v75 offset1:16
	ds_read2_b64 v[40:43], v67 offset1:16
	v_add_u32_e32 v63, 0x800, v15
	v_xad_u32 v15, v13, 13, v10
	v_lshl_add_u32 v15, v15, 3, 0
	v_add_u32_e32 v62, 0x800, v15
	v_xad_u32 v15, v13, 14, v10
	v_xad_u32 v10, v13, 15, v10
	ds_read2_b64 v[22:25], v74 offset0:32 offset1:48
	ds_read2_b64 v[48:51], v66 offset0:32 offset1:48
	v_lshl_add_u32 v15, v15, 3, 0
	v_lshl_add_u32 v10, v10, 3, 0
	v_add_u32_e32 v15, 0x800, v15
	v_add_u32_e32 v13, 0x800, v10
	ds_read2_b64 v[26:29], v73 offset0:64 offset1:80
	ds_read2_b64 v[58:61], v72 offset0:96 offset1:112
	ds_read2_b64 v[76:79], v71 offset0:128 offset1:144
	ds_read2_b64 v[80:83], v70 offset0:160 offset1:176
	ds_read2_b64 v[84:87], v69 offset0:192 offset1:208
	ds_read2_b64 v[88:91], v68 offset0:224 offset1:240
	ds_read2_b64 v[54:57], v65 offset0:64 offset1:80
	ds_read2_b64 v[92:95], v64 offset0:96 offset1:112
	ds_read2_b64 v[96:99], v63 offset0:128 offset1:144
	ds_read2_b64 v[100:103], v62 offset0:160 offset1:176
	ds_read2_b64 v[104:107], v15 offset0:192 offset1:208
	ds_read2_b64 v[108:111], v13 offset0:224 offset1:240
	s_waitcnt lgkmcnt(14)
	v_pk_add_f32 v[112:113], v[18:19], v[40:41]
	v_pk_add_f32 v[40:41], v[18:19], v[40:41] neg_lo:[0,1] neg_hi:[0,1]
	v_pk_add_f32 v[18:19], v[20:21], v[42:43]
	v_pk_add_f32 v[20:21], v[20:21], v[42:43] neg_lo:[0,1] neg_hi:[0,1]
	v_mov_b32_e32 v30, v164
	v_mov_b32_e32 v32, v165
	v_mov_b32_e32 v34, v166
	v_mov_b32_e32 v10, v167
	v_mov_b32_e32 v38, v168
	v_mov_b32_e32 v36, v169
	v_mov_b32_e32 v46, v170
	v_mov_b32_e32 v31, v171
	v_pk_mul_f32 v[42:43], v[20:21], v[46:47] op_sel:[1,0] op_sel_hi:[0,0] neg_lo:[1,1] neg_hi:[0,1]
	s_nop 0
	v_pk_fma_f32 v[44:45], v[20:21], v[30:31], v[42:43] op_sel_hi:[1,0,1]
	s_waitcnt lgkmcnt(12)
	v_pk_add_f32 v[20:21], v[22:23], v[48:49]
	v_pk_add_f32 v[22:23], v[22:23], v[48:49] neg_lo:[0,1] neg_hi:[0,1]
	s_nop 0
	v_pk_mul_f32 v[42:43], v[22:23], v[36:37] op_sel:[1,0] op_sel_hi:[0,0] neg_lo:[1,1] neg_hi:[0,1]
	s_nop 0
	v_pk_fma_f32 v[48:49], v[22:23], v[32:33], v[42:43] op_sel_hi:[1,0,1]
	v_pk_add_f32 v[22:23], v[24:25], v[50:51]
	v_pk_add_f32 v[24:25], v[24:25], v[50:51] neg_lo:[0,1] neg_hi:[0,1]
	s_nop 0
	v_pk_mul_f32 v[42:43], v[24:25], v[38:39] op_sel:[1,0] op_sel_hi:[0,0] neg_lo:[1,1] neg_hi:[0,1]
	s_nop 0
	v_pk_fma_f32 v[52:53], v[24:25], v[34:35], v[42:43] op_sel_hi:[1,0,1]
	s_waitcnt lgkmcnt(5)
	v_pk_add_f32 v[24:25], v[26:27], v[54:55]
	v_pk_add_f32 v[26:27], v[26:27], v[54:55] neg_lo:[0,1] neg_hi:[0,1]
	s_nop 0
	v_pk_mul_f32 v[42:43], v[26:27], v[10:11] op_sel:[1,0] op_sel_hi:[0,0] neg_lo:[1,1] neg_hi:[0,1]
	s_nop 0
	v_pk_fma_f32 v[54:55], v[26:27], v[10:11], v[42:43] op_sel_hi:[1,0,1]
	v_pk_add_f32 v[26:27], v[28:29], v[56:57]
	v_pk_add_f32 v[28:29], v[28:29], v[56:57] neg_lo:[0,1] neg_hi:[0,1]
	s_nop 0
	v_pk_mul_f32 v[42:43], v[28:29], v[38:39] op_sel_hi:[1,0]
	s_nop 0
	v_pk_fma_f32 v[56:57], v[28:29], v[34:35], v[42:43] op_sel:[1,0,0] op_sel_hi:[0,0,1] neg_lo:[1,1,0] neg_hi:[0,1,0]
	s_waitcnt lgkmcnt(4)
	v_pk_add_f32 v[42:43], v[58:59], v[92:93] neg_lo:[0,1] neg_hi:[0,1]
	v_pk_add_f32 v[28:29], v[58:59], v[92:93]
	v_pk_mul_f32 v[50:51], v[42:43], v[36:37] op_sel_hi:[1,0]
	s_nop 0
	v_pk_fma_f32 v[58:59], v[42:43], v[32:33], v[50:51] op_sel:[1,0,0] op_sel_hi:[0,0,1] neg_lo:[1,1,0] neg_hi:[0,1,0]
	v_pk_add_f32 v[50:51], v[60:61], v[94:95] neg_lo:[0,1] neg_hi:[0,1]
	v_pk_add_f32 v[42:43], v[60:61], v[94:95]
	v_pk_mul_f32 v[60:61], v[50:51], v[46:47] op_sel_hi:[1,0]
	v_xor_b32_e32 v92, 0x80000000, v51
	v_mov_b32_e32 v93, v50
	s_waitcnt lgkmcnt(3)
	v_pk_add_f32 v[50:51], v[76:77], v[96:97]
	v_pk_add_f32 v[76:77], v[76:77], v[96:97] neg_lo:[0,1] neg_hi:[0,1]
	v_pk_fma_f32 v[60:61], v[92:93], v[30:31], v[60:61] op_sel_hi:[1,0,1] neg_lo:[0,1,0] neg_hi:[0,1,0]
	v_xor_b32_e32 v93, 0x80000000, v76
	v_mov_b32_e32 v92, v77
	v_pk_add_f32 v[76:77], v[78:79], v[98:99]
	v_pk_add_f32 v[78:79], v[78:79], v[98:99] neg_lo:[0,1] neg_hi:[0,1]
	s_nop 0
	v_pk_mul_f32 v[94:95], v[78:79], v[46:47] op_sel_hi:[1,0] neg_lo:[0,1] neg_hi:[0,1]
	s_nop 0
	v_pk_fma_f32 v[78:79], v[78:79], v[30:31], v[94:95] op_sel:[1,0,0] op_sel_hi:[0,0,1] neg_lo:[1,1,0] neg_hi:[0,1,0]
	s_waitcnt lgkmcnt(2)
	v_pk_add_f32 v[94:95], v[80:81], v[100:101]
	v_pk_add_f32 v[80:81], v[80:81], v[100:101] neg_lo:[0,1] neg_hi:[0,1]
	s_nop 0
	v_pk_mul_f32 v[96:97], v[80:81], v[36:37] op_sel_hi:[1,0] neg_lo:[0,1] neg_hi:[0,1]
	s_nop 0
	v_pk_fma_f32 v[80:81], v[80:81], v[32:33], v[96:97] op_sel:[1,0,0] op_sel_hi:[0,0,1] neg_lo:[1,1,0] neg_hi:[0,1,0]
	v_pk_add_f32 v[96:97], v[82:83], v[102:103]
	v_pk_add_f32 v[82:83], v[82:83], v[102:103] neg_lo:[0,1] neg_hi:[0,1]
	s_nop 0
	v_pk_mul_f32 v[98:99], v[82:83], v[38:39] op_sel_hi:[1,0] neg_lo:[0,1] neg_hi:[0,1]
	s_nop 0
	v_pk_fma_f32 v[82:83], v[82:83], v[34:35], v[98:99] op_sel:[1,0,0] op_sel_hi:[0,0,1] neg_lo:[1,1,0] neg_hi:[0,1,0]
	s_waitcnt lgkmcnt(1)
	v_pk_add_f32 v[98:99], v[84:85], v[104:105]
	v_pk_add_f32 v[84:85], v[84:85], v[104:105] neg_lo:[0,1] neg_hi:[0,1]
	s_nop 0
	v_pk_mul_f32 v[100:101], v[84:85], v[10:11] op_sel:[1,0] op_sel_hi:[0,0] neg_lo:[1,1] neg_hi:[0,1]
	s_nop 0
	v_pk_fma_f32 v[84:85], v[84:85], v[10:11], v[100:101] op_sel_hi:[1,0,1] neg_lo:[0,1,0] neg_hi:[0,1,0]
	v_pk_add_f32 v[100:101], v[86:87], v[106:107]
	v_pk_add_f32 v[86:87], v[86:87], v[106:107] neg_lo:[0,1] neg_hi:[0,1]
	s_nop 0
	v_pk_mul_f32 v[38:39], v[86:87], v[38:39] op_sel:[1,0] op_sel_hi:[0,0] neg_lo:[1,1] neg_hi:[0,1]
	s_nop 0
	v_pk_fma_f32 v[86:87], v[86:87], v[34:35], v[38:39] op_sel_hi:[1,0,1] neg_lo:[0,1,0] neg_hi:[0,1,0]
	s_waitcnt lgkmcnt(0)
	v_pk_add_f32 v[38:39], v[88:89], v[108:109] neg_lo:[0,1] neg_hi:[0,1]
	v_pk_add_f32 v[34:35], v[88:89], v[108:109]
	v_pk_mul_f32 v[88:89], v[38:39], v[36:37] op_sel:[1,0] op_sel_hi:[0,0] neg_lo:[1,1] neg_hi:[0,1]
	s_nop 0
	v_pk_fma_f32 v[88:89], v[38:39], v[32:33], v[88:89] op_sel_hi:[1,0,1] neg_lo:[0,1,0] neg_hi:[0,1,0]
	v_pk_add_f32 v[38:39], v[90:91], v[110:111]
	v_pk_add_f32 v[90:91], v[90:91], v[110:111] neg_lo:[0,1] neg_hi:[0,1]
	s_nop 0
	v_pk_mul_f32 v[46:47], v[90:91], v[46:47] op_sel:[1,0] op_sel_hi:[0,0] neg_lo:[1,1] neg_hi:[0,1]
	s_nop 0
	v_pk_fma_f32 v[90:91], v[90:91], v[30:31], v[46:47] op_sel_hi:[1,0,1] neg_lo:[0,1,0] neg_hi:[0,1,0]
	v_pk_add_f32 v[46:47], v[18:19], v[76:77]
	v_pk_add_f32 v[18:19], v[18:19], v[76:77] neg_lo:[0,1] neg_hi:[0,1]
	v_pk_add_f32 v[30:31], v[112:113], v[50:51]
	v_pk_mul_f32 v[76:77], v[18:19], v[36:37] op_sel:[1,0] op_sel_hi:[0,0] neg_lo:[1,1] neg_hi:[0,1]
	v_pk_add_f32 v[50:51], v[112:113], v[50:51] neg_lo:[0,1] neg_hi:[0,1]
	v_pk_fma_f32 v[76:77], v[18:19], v[32:33], v[76:77] op_sel_hi:[1,0,1]
	v_pk_add_f32 v[18:19], v[20:21], v[94:95]
	v_pk_add_f32 v[20:21], v[20:21], v[94:95] neg_lo:[0,1] neg_hi:[0,1]
	s_nop 0
	v_pk_mul_f32 v[94:95], v[20:21], v[10:11] op_sel:[1,0] op_sel_hi:[0,0] neg_lo:[1,1] neg_hi:[0,1]
	s_nop 0
	v_pk_fma_f32 v[20:21], v[20:21], v[10:11], v[94:95] op_sel_hi:[1,0,1]
	v_pk_add_f32 v[94:95], v[22:23], v[96:97]
	v_pk_add_f32 v[22:23], v[22:23], v[96:97] neg_lo:[0,1] neg_hi:[0,1]
	s_nop 0
	v_pk_mul_f32 v[96:97], v[22:23], v[36:37] op_sel_hi:[1,0]
	v_xor_b32_e32 v102, 0x80000000, v23
	v_mov_b32_e32 v103, v22
	v_pk_add_f32 v[22:23], v[24:25], v[98:99]
	v_pk_add_f32 v[24:25], v[24:25], v[98:99] neg_lo:[0,1] neg_hi:[0,1]
	v_pk_fma_f32 v[96:97], v[102:103], v[32:33], v[96:97] op_sel_hi:[1,0,1] neg_lo:[0,1,0] neg_hi:[0,1,0]
	v_xor_b32_e32 v99, 0x80000000, v24
	v_mov_b32_e32 v98, v25
	v_pk_add_f32 v[24:25], v[26:27], v[100:101]
	v_pk_add_f32 v[26:27], v[26:27], v[100:101] neg_lo:[0,1] neg_hi:[0,1]
	s_nop 0
	v_pk_mul_f32 v[100:101], v[26:27], v[36:37] op_sel_hi:[1,0] neg_lo:[0,1] neg_hi:[0,1]
	v_xor_b32_e32 v102, 0x80000000, v27
	v_mov_b32_e32 v103, v26
	v_pk_add_f32 v[26:27], v[28:29], v[34:35]
	v_pk_add_f32 v[28:29], v[28:29], v[34:35] neg_lo:[0,1] neg_hi:[0,1]
	v_pk_fma_f32 v[100:101], v[102:103], v[32:33], v[100:101] op_sel_hi:[1,0,1] neg_lo:[0,1,0] neg_hi:[0,1,0]
	v_pk_mul_f32 v[34:35], v[28:29], v[10:11] op_sel:[1,0] op_sel_hi:[0,0] neg_lo:[1,1] neg_hi:[0,1]
	v_pk_add_f32 v[102:103], v[30:31], v[22:23] neg_lo:[0,1] neg_hi:[0,1]
	v_pk_fma_f32 v[28:29], v[28:29], v[10:11], v[34:35] op_sel_hi:[1,0,1] neg_lo:[0,1,0] neg_hi:[0,1,0]
	v_pk_add_f32 v[34:35], v[42:43], v[38:39]
	v_pk_add_f32 v[38:39], v[42:43], v[38:39] neg_lo:[0,1] neg_hi:[0,1]
	s_nop 0
	v_pk_mul_f32 v[42:43], v[38:39], v[36:37] op_sel:[1,0] op_sel_hi:[0,0] neg_lo:[1,1] neg_hi:[0,1]
	s_nop 0
	v_pk_fma_f32 v[42:43], v[38:39], v[32:33], v[42:43] op_sel_hi:[1,0,1] neg_lo:[0,1,0] neg_hi:[0,1,0]
	v_pk_add_f32 v[38:39], v[30:31], v[22:23]
	v_pk_add_f32 v[22:23], v[46:47], v[24:25]
	v_pk_add_f32 v[24:25], v[46:47], v[24:25] neg_lo:[0,1] neg_hi:[0,1]
	s_nop 0
	v_pk_mul_f32 v[30:31], v[24:25], v[10:11] op_sel:[1,0] op_sel_hi:[0,0] neg_lo:[1,1] neg_hi:[0,1]
	s_nop 0
	v_pk_fma_f32 v[24:25], v[24:25], v[10:11], v[30:31] op_sel_hi:[1,0,1]
	v_pk_add_f32 v[30:31], v[18:19], v[26:27]
	v_pk_add_f32 v[18:19], v[18:19], v[26:27] neg_lo:[0,1] neg_hi:[0,1]
	s_nop 0
	v_xor_b32_e32 v27, 0x80000000, v18
	v_mov_b32_e32 v26, v19
	v_pk_add_f32 v[18:19], v[94:95], v[34:35]
	v_pk_add_f32 v[34:35], v[94:95], v[34:35] neg_lo:[0,1] neg_hi:[0,1]
	s_nop 0
	v_pk_mul_f32 v[46:47], v[34:35], v[10:11] op_sel:[1,0] op_sel_hi:[0,0] neg_lo:[1,1] neg_hi:[0,1]
	s_nop 0
	v_pk_fma_f32 v[34:35], v[34:35], v[10:11], v[46:47] op_sel_hi:[1,0,1] neg_lo:[0,1,0] neg_hi:[0,1,0]
	v_pk_add_f32 v[46:47], v[38:39], v[30:31]
	v_pk_add_f32 v[38:39], v[38:39], v[30:31] neg_lo:[0,1] neg_hi:[0,1]
	v_pk_add_f32 v[30:31], v[22:23], v[18:19]
	v_pk_add_f32 v[18:19], v[22:23], v[18:19] neg_lo:[0,1] neg_hi:[0,1]
	v_pk_add_f32 v[94:95], v[46:47], v[30:31]
	v_xor_b32_e32 v23, 0x80000000, v18
	v_mov_b32_e32 v22, v19
	v_pk_add_f32 v[18:19], v[102:103], v[26:27]
	v_pk_add_f32 v[102:103], v[102:103], v[26:27] neg_lo:[0,1] neg_hi:[0,1]
	v_pk_add_f32 v[26:27], v[24:25], v[34:35]
	v_pk_add_f32 v[24:25], v[24:25], v[34:35] neg_lo:[0,1] neg_hi:[0,1]
	v_pk_add_f32 v[30:31], v[46:47], v[30:31] neg_lo:[0,1] neg_hi:[0,1]
	v_xor_b32_e32 v35, 0x80000000, v24
	v_mov_b32_e32 v34, v25
	v_pk_add_f32 v[24:25], v[50:51], v[98:99]
	v_pk_add_f32 v[98:99], v[50:51], v[98:99] neg_lo:[0,1] neg_hi:[0,1]
	v_pk_add_f32 v[50:51], v[76:77], v[100:101] neg_lo:[0,1] neg_hi:[0,1]
	v_pk_add_f32 v[46:47], v[38:39], v[22:23]
	v_pk_add_f32 v[22:23], v[38:39], v[22:23] neg_lo:[0,1] neg_hi:[0,1]
	v_pk_add_f32 v[104:105], v[18:19], v[26:27]
	v_pk_add_f32 v[26:27], v[18:19], v[26:27] neg_lo:[0,1] neg_hi:[0,1]
	v_pk_add_f32 v[38:39], v[102:103], v[34:35]
	v_pk_add_f32 v[18:19], v[102:103], v[34:35] neg_lo:[0,1] neg_hi:[0,1]
	v_pk_add_f32 v[34:35], v[76:77], v[100:101]
	v_pk_mul_f32 v[76:77], v[10:11], v[50:51] op_sel:[0,1] op_sel_hi:[0,0] neg_lo:[1,1] neg_hi:[1,0]
	v_pk_fma_f32 v[76:77], v[10:11], v[50:51], v[76:77] op_sel_hi:[0,1,1]
	v_pk_add_f32 v[50:51], v[20:21], v[28:29]
	v_pk_add_f32 v[20:21], v[20:21], v[28:29] neg_lo:[0,1] neg_hi:[0,1]
	s_nop 0
	v_xor_b32_e32 v29, 0x80000000, v20
	v_mov_b32_e32 v28, v21
	v_pk_add_f32 v[20:21], v[96:97], v[42:43]
	v_pk_add_f32 v[42:43], v[96:97], v[42:43] neg_lo:[0,1] neg_hi:[0,1]
	s_nop 0
	v_pk_mul_f32 v[96:97], v[10:11], v[42:43] op_sel:[0,1] op_sel_hi:[0,0] neg_lo:[1,1] neg_hi:[1,0]
	v_pk_fma_f32 v[42:43], v[10:11], v[42:43], v[96:97] op_sel_hi:[0,1,1] neg_lo:[1,0,0] neg_hi:[1,0,0]
	v_pk_add_f32 v[96:97], v[24:25], v[50:51]
	v_pk_add_f32 v[24:25], v[24:25], v[50:51] neg_lo:[0,1] neg_hi:[0,1]
	v_pk_add_f32 v[50:51], v[34:35], v[20:21]
	v_pk_add_f32 v[20:21], v[34:35], v[20:21] neg_lo:[0,1] neg_hi:[0,1]
	v_pk_add_f32 v[102:103], v[96:97], v[50:51]
	v_xor_b32_e32 v101, 0x80000000, v20
	v_mov_b32_e32 v100, v21
	v_pk_add_f32 v[34:35], v[96:97], v[50:51] neg_lo:[0,1] neg_hi:[0,1]
	v_pk_add_f32 v[20:21], v[98:99], v[28:29]
	v_pk_add_f32 v[96:97], v[98:99], v[28:29] neg_lo:[0,1] neg_hi:[0,1]
	v_pk_add_f32 v[28:29], v[76:77], v[42:43]
	v_pk_add_f32 v[42:43], v[76:77], v[42:43] neg_lo:[0,1] neg_hi:[0,1]
	v_pk_add_f32 v[98:99], v[20:21], v[28:29]
	v_xor_b32_e32 v77, 0x80000000, v42
	v_mov_b32_e32 v76, v43
	v_pk_add_f32 v[28:29], v[20:21], v[28:29] neg_lo:[0,1] neg_hi:[0,1]
	v_pk_add_f32 v[42:43], v[96:97], v[76:77]
	v_pk_add_f32 v[20:21], v[96:97], v[76:77] neg_lo:[0,1] neg_hi:[0,1]
	v_pk_add_f32 v[76:77], v[40:41], v[92:93]
	v_pk_add_f32 v[92:93], v[40:41], v[92:93] neg_lo:[0,1] neg_hi:[0,1]
	v_pk_add_f32 v[40:41], v[44:45], v[78:79]
	v_pk_add_f32 v[44:45], v[44:45], v[78:79] neg_lo:[0,1] neg_hi:[0,1]
	v_pk_add_f32 v[50:51], v[24:25], v[100:101]
	v_pk_mul_f32 v[78:79], v[36:37], v[44:45] op_sel:[0,1] op_sel_hi:[0,0] neg_lo:[1,1] neg_hi:[1,0]
	v_pk_fma_f32 v[44:45], v[32:33], v[44:45], v[78:79] op_sel_hi:[0,1,1]
	v_pk_add_f32 v[78:79], v[48:49], v[80:81]
	v_pk_add_f32 v[48:49], v[48:49], v[80:81] neg_lo:[0,1] neg_hi:[0,1]
	v_pk_add_f32 v[24:25], v[24:25], v[100:101] neg_lo:[0,1] neg_hi:[0,1]
	v_pk_mul_f32 v[80:81], v[10:11], v[48:49] op_sel:[0,1] op_sel_hi:[0,0] neg_lo:[1,1] neg_hi:[1,0]
	v_pk_fma_f32 v[80:81], v[10:11], v[48:49], v[80:81] op_sel_hi:[0,1,1]
	v_pk_add_f32 v[48:49], v[52:53], v[82:83]
	v_pk_add_f32 v[52:53], v[52:53], v[82:83] neg_lo:[0,1] neg_hi:[0,1]
	s_nop 0
	v_pk_mul_f32 v[82:83], v[32:33], v[52:53] op_sel:[0,1] op_sel_hi:[0,0] neg_lo:[1,1] neg_hi:[1,0]
	v_pk_fma_f32 v[52:53], v[36:37], v[52:53], v[82:83] op_sel_hi:[0,1,1]
	v_pk_add_f32 v[82:83], v[54:55], v[84:85]
	v_pk_add_f32 v[54:55], v[54:55], v[84:85] neg_lo:[0,1] neg_hi:[0,1]
	s_nop 0
	v_xor_b32_e32 v85, 0x80000000, v54
	v_mov_b32_e32 v84, v55
	v_pk_add_f32 v[54:55], v[56:57], v[86:87]
	v_pk_add_f32 v[56:57], v[56:57], v[86:87] neg_lo:[0,1] neg_hi:[0,1]
	s_nop 0
	v_pk_mul_f32 v[86:87], v[32:33], v[56:57] op_sel:[0,1] op_sel_hi:[0,0] neg_lo:[1,1] neg_hi:[1,0]
	v_pk_fma_f32 v[56:57], v[36:37], v[56:57], v[86:87] op_sel_hi:[0,1,1] neg_lo:[1,0,0] neg_hi:[1,0,0]
	v_pk_add_f32 v[86:87], v[58:59], v[88:89]
	v_pk_add_f32 v[58:59], v[58:59], v[88:89] neg_lo:[0,1] neg_hi:[0,1]
	s_nop 0
	v_pk_mul_f32 v[88:89], v[10:11], v[58:59] op_sel:[0,1] op_sel_hi:[0,0] neg_lo:[1,1] neg_hi:[1,0]
	v_pk_fma_f32 v[58:59], v[10:11], v[58:59], v[88:89] op_sel_hi:[0,1,1] neg_lo:[1,0,0] neg_hi:[1,0,0]
	v_pk_add_f32 v[88:89], v[60:61], v[90:91]
	v_pk_add_f32 v[60:61], v[60:61], v[90:91] neg_lo:[0,1] neg_hi:[0,1]
	s_nop 0
	v_pk_mul_f32 v[36:37], v[36:37], v[60:61] op_sel:[0,1] op_sel_hi:[0,0] neg_lo:[1,1] neg_hi:[1,0]
	v_pk_fma_f32 v[36:37], v[32:33], v[60:61], v[36:37] op_sel_hi:[0,1,1] neg_lo:[1,0,0] neg_hi:[1,0,0]
	v_pk_add_f32 v[32:33], v[76:77], v[82:83]
	v_pk_add_f32 v[60:61], v[76:77], v[82:83] neg_lo:[0,1] neg_hi:[0,1]
	v_pk_add_f32 v[76:77], v[54:55], v[40:41]
	v_pk_add_f32 v[40:41], v[40:41], v[54:55] neg_lo:[0,1] neg_hi:[0,1]
	s_nop 0
	v_pk_mul_f32 v[54:55], v[10:11], v[40:41] op_sel:[0,1] op_sel_hi:[0,0] neg_lo:[1,1] neg_hi:[1,0]
	v_pk_fma_f32 v[54:55], v[10:11], v[40:41], v[54:55] op_sel_hi:[0,1,1]
	v_pk_add_f32 v[40:41], v[78:79], v[86:87]
	v_pk_add_f32 v[78:79], v[78:79], v[86:87] neg_lo:[0,1] neg_hi:[0,1]
	s_nop 0
	v_xor_b32_e32 v83, 0x80000000, v78
	v_mov_b32_e32 v82, v79
	v_pk_add_f32 v[78:79], v[48:49], v[88:89]
	v_pk_add_f32 v[48:49], v[48:49], v[88:89] neg_lo:[0,1] neg_hi:[0,1]
	v_pk_add_f32 v[88:89], v[76:77], v[78:79]
	v_pk_mul_f32 v[86:87], v[10:11], v[48:49] op_sel:[0,1] op_sel_hi:[0,0] neg_lo:[1,1] neg_hi:[1,0]
	v_pk_fma_f32 v[48:49], v[10:11], v[48:49], v[86:87] op_sel_hi:[0,1,1] neg_lo:[1,0,0] neg_hi:[1,0,0]
	v_pk_add_f32 v[86:87], v[32:33], v[40:41]
	v_pk_add_f32 v[32:33], v[32:33], v[40:41] neg_lo:[0,1] neg_hi:[0,1]
	v_pk_add_f32 v[40:41], v[76:77], v[78:79] neg_lo:[0,1] neg_hi:[0,1]
	v_pk_add_f32 v[78:79], v[86:87], v[88:89] neg_lo:[0,1] neg_hi:[0,1]
	v_pk_add_f32 v[90:91], v[32:33], v[40:41] op_sel:[0,1] op_sel_hi:[1,0] neg_hi:[0,1]
	v_pk_add_f32 v[40:41], v[32:33], v[40:41] op_sel:[0,1] op_sel_hi:[1,0] neg_lo:[0,1]
	v_pk_add_f32 v[76:77], v[54:55], v[48:49]
	v_pk_add_f32 v[48:49], v[54:55], v[48:49] neg_lo:[0,1] neg_hi:[0,1]
	v_pk_add_f32 v[32:33], v[60:61], v[82:83]
	v_pk_add_f32 v[60:61], v[60:61], v[82:83] neg_lo:[0,1] neg_hi:[0,1]
	v_xor_b32_e32 v55, 0x80000000, v48
	v_mov_b32_e32 v54, v49
	v_pk_add_f32 v[82:83], v[32:33], v[76:77]
	v_pk_add_f32 v[48:49], v[32:33], v[76:77] neg_lo:[0,1] neg_hi:[0,1]
	v_pk_add_f32 v[76:77], v[60:61], v[54:55]
	v_pk_add_f32 v[32:33], v[60:61], v[54:55] neg_lo:[0,1] neg_hi:[0,1]
	v_pk_add_f32 v[54:55], v[92:93], v[84:85]
	v_pk_add_f32 v[60:61], v[92:93], v[84:85] neg_lo:[0,1] neg_hi:[0,1]
	v_pk_add_f32 v[84:85], v[56:57], v[44:45]
	v_pk_add_f32 v[44:45], v[44:45], v[56:57] neg_lo:[0,1] neg_hi:[0,1]
	v_pk_add_f32 v[86:87], v[86:87], v[88:89]
	v_pk_mul_f32 v[56:57], v[10:11], v[44:45] op_sel:[0,1] op_sel_hi:[0,0] neg_lo:[1,1] neg_hi:[1,0]
	v_pk_fma_f32 v[56:57], v[10:11], v[44:45], v[56:57] op_sel_hi:[0,1,1]
	v_pk_add_f32 v[44:45], v[80:81], v[58:59]
	v_pk_add_f32 v[58:59], v[80:81], v[58:59] neg_lo:[0,1] neg_hi:[0,1]
	s_nop 0
	v_xor_b32_e32 v81, 0x80000000, v58
	v_mov_b32_e32 v80, v59
	v_pk_add_f32 v[58:59], v[52:53], v[36:37]
	v_pk_add_f32 v[36:37], v[52:53], v[36:37] neg_lo:[0,1] neg_hi:[0,1]
	s_nop 0
	v_pk_mul_f32 v[52:53], v[10:11], v[36:37] op_sel:[0,1] op_sel_hi:[0,0] neg_lo:[1,1] neg_hi:[1,0]
	v_pk_fma_f32 v[36:37], v[10:11], v[36:37], v[52:53] op_sel_hi:[0,1,1] neg_lo:[1,0,0] neg_hi:[1,0,0]
	v_pk_add_f32 v[52:53], v[54:55], v[44:45]
	v_pk_add_f32 v[44:45], v[54:55], v[44:45] neg_lo:[0,1] neg_hi:[0,1]
	v_pk_add_f32 v[54:55], v[84:85], v[58:59]
	v_pk_add_f32 v[58:59], v[84:85], v[58:59] neg_lo:[0,1] neg_hi:[0,1]
	s_nop 0
	v_xor_b32_e32 v85, 0x80000000, v58
	v_mov_b32_e32 v84, v59
	v_pk_add_f32 v[58:59], v[52:53], v[54:55]
	v_pk_add_f32 v[52:53], v[52:53], v[54:55] neg_lo:[0,1] neg_hi:[0,1]
	v_pk_add_f32 v[54:55], v[44:45], v[84:85]
	v_pk_add_f32 v[44:45], v[44:45], v[84:85] neg_lo:[0,1] neg_hi:[0,1]
	v_pk_add_f32 v[84:85], v[60:61], v[80:81]
	v_pk_add_f32 v[60:61], v[60:61], v[80:81] neg_lo:[0,1] neg_hi:[0,1]
	v_pk_add_f32 v[80:81], v[56:57], v[36:37]
	v_pk_add_f32 v[36:37], v[56:57], v[36:37] neg_lo:[0,1] neg_hi:[0,1]
	v_pk_add_f32 v[92:93], v[84:85], v[80:81]
	v_pk_add_f32 v[80:81], v[84:85], v[80:81] neg_lo:[0,1] neg_hi:[0,1]
	v_pk_add_f32 v[84:85], v[60:61], v[36:37] op_sel:[0,1] op_sel_hi:[1,0] neg_hi:[0,1]
	v_pk_add_f32 v[36:37], v[60:61], v[36:37] op_sel:[0,1] op_sel_hi:[1,0] neg_lo:[0,1]
	v_pk_fma_f32 v[60:61], v[16:17], s[90:91], v[16:17] op_sel:[1,0,0] op_sel_hi:[0,1,1]
	v_pk_mul_f32 v[56:57], v[94:95], s[14:15] op_sel:[1,0] neg_lo:[1,0]
	v_pk_mul_f32 v[88:89], v[60:61], v[86:87] op_sel:[1,1] op_sel_hi:[0,1] neg_lo:[0,1]
	v_pk_fma_f32 v[56:57], v[94:95], s[94:95], v[56:57] op_sel_hi:[0,1,1]
	v_pk_fma_f32 v[86:87], v[60:61], v[86:87], v[88:89] op_sel_hi:[1,0,1]
	ds_write2_b64 v75, v[56:57], v[86:87] offset1:16
	v_pk_mul_f32 v[56:57], v[16:17], v[60:61] op_sel:[1,1] op_sel_hi:[0,1] neg_lo:[0,1]
	v_pk_fma_f32 v[56:57], v[16:17], v[60:61], v[56:57] op_sel_hi:[1,0,1]
	s_nop 0
	v_pk_mul_f32 v[60:61], v[56:57], v[102:103] op_sel:[1,1] op_sel_hi:[0,1] neg_lo:[0,1]
	v_pk_mul_f32 v[86:87], v[16:17], v[56:57] op_sel:[1,1] op_sel_hi:[0,1] neg_lo:[0,1]
	v_pk_fma_f32 v[60:61], v[56:57], v[102:103], v[60:61] op_sel_hi:[1,0,1]
	v_pk_fma_f32 v[56:57], v[16:17], v[56:57], v[86:87] op_sel_hi:[1,0,1]
	s_nop 0
	v_pk_mul_f32 v[86:87], v[56:57], v[58:59] op_sel:[1,1] op_sel_hi:[0,1] neg_lo:[0,1]
	v_pk_fma_f32 v[58:59], v[56:57], v[58:59], v[86:87] op_sel_hi:[1,0,1]
	ds_write2_b64 v74, v[60:61], v[58:59] offset0:32 offset1:48
	v_pk_mul_f32 v[58:59], v[16:17], v[56:57] op_sel:[1,1] op_sel_hi:[0,1] neg_lo:[0,1]
	v_pk_fma_f32 v[56:57], v[16:17], v[56:57], v[58:59] op_sel_hi:[1,0,1]
	s_nop 0
	v_pk_mul_f32 v[58:59], v[56:57], v[104:105] op_sel:[1,1] op_sel_hi:[0,1] neg_lo:[0,1]
	v_pk_mul_f32 v[60:61], v[16:17], v[56:57] op_sel:[1,1] op_sel_hi:[0,1] neg_lo:[0,1]
	v_pk_fma_f32 v[58:59], v[56:57], v[104:105], v[58:59] op_sel_hi:[1,0,1]
	v_pk_fma_f32 v[56:57], v[16:17], v[56:57], v[60:61] op_sel_hi:[1,0,1]
	s_nop 0
	v_pk_mul_f32 v[60:61], v[56:57], v[82:83] op_sel:[1,1] op_sel_hi:[0,1] neg_lo:[0,1]
	v_pk_fma_f32 v[60:61], v[56:57], v[82:83], v[60:61] op_sel_hi:[1,0,1]
	ds_write2_b64 v73, v[58:59], v[60:61] offset0:64 offset1:80
	v_pk_mul_f32 v[58:59], v[16:17], v[56:57] op_sel:[1,1] op_sel_hi:[0,1] neg_lo:[0,1]
	v_pk_fma_f32 v[56:57], v[16:17], v[56:57], v[58:59] op_sel_hi:[1,0,1]
	s_nop 0
	v_pk_mul_f32 v[58:59], v[56:57], v[98:99] op_sel:[1,1] op_sel_hi:[0,1] neg_lo:[0,1]
	v_pk_mul_f32 v[60:61], v[16:17], v[56:57] op_sel:[1,1] op_sel_hi:[0,1] neg_lo:[0,1]
	v_pk_fma_f32 v[58:59], v[56:57], v[98:99], v[58:59] op_sel_hi:[1,0,1]
	v_pk_fma_f32 v[56:57], v[16:17], v[56:57], v[60:61] op_sel_hi:[1,0,1]
	s_nop 0
	v_pk_mul_f32 v[60:61], v[56:57], v[92:93] op_sel:[1,1] op_sel_hi:[0,1] neg_lo:[0,1]
	v_pk_fma_f32 v[60:61], v[56:57], v[92:93], v[60:61] op_sel_hi:[1,0,1]
	ds_write2_b64 v72, v[58:59], v[60:61] offset0:96 offset1:112
	v_pk_mul_f32 v[58:59], v[16:17], v[56:57] op_sel:[1,1] op_sel_hi:[0,1] neg_lo:[0,1]
	v_pk_fma_f32 v[56:57], v[16:17], v[56:57], v[58:59] op_sel_hi:[1,0,1]
	s_nop 0
	v_pk_mul_f32 v[58:59], v[56:57], v[46:47] op_sel:[1,1] op_sel_hi:[0,1] neg_lo:[0,1]
	v_pk_fma_f32 v[46:47], v[56:57], v[46:47], v[58:59] op_sel_hi:[1,0,1]
	v_pk_mul_f32 v[58:59], v[16:17], v[56:57] op_sel:[1,1] op_sel_hi:[0,1] neg_lo:[0,1]
	v_pk_fma_f32 v[56:57], v[16:17], v[56:57], v[58:59] op_sel_hi:[1,0,1]
	s_nop 0
	v_pk_mul_f32 v[58:59], v[56:57], v[90:91] op_sel:[1,1] op_sel_hi:[0,1] neg_lo:[0,1]
	v_pk_fma_f32 v[58:59], v[56:57], v[90:91], v[58:59] op_sel_hi:[1,0,1]
	ds_write2_b64 v71, v[46:47], v[58:59] offset0:128 offset1:144
	v_pk_mul_f32 v[46:47], v[16:17], v[56:57] op_sel:[1,1] op_sel_hi:[0,1] neg_lo:[0,1]
	v_pk_fma_f32 v[46:47], v[16:17], v[56:57], v[46:47] op_sel_hi:[1,0,1]
	s_nop 0
	v_pk_mul_f32 v[56:57], v[46:47], v[50:51] op_sel:[1,1] op_sel_hi:[0,1] neg_lo:[0,1]
	v_pk_fma_f32 v[50:51], v[46:47], v[50:51], v[56:57] op_sel_hi:[1,0,1]
	v_pk_mul_f32 v[56:57], v[16:17], v[46:47] op_sel:[1,1] op_sel_hi:[0,1] neg_lo:[0,1]
	v_pk_fma_f32 v[46:47], v[16:17], v[46:47], v[56:57] op_sel_hi:[1,0,1]
	s_nop 0
	v_pk_mul_f32 v[56:57], v[46:47], v[54:55] op_sel:[1,1] op_sel_hi:[0,1] neg_lo:[0,1]
	v_pk_fma_f32 v[54:55], v[46:47], v[54:55], v[56:57] op_sel_hi:[1,0,1]
	ds_write2_b64 v70, v[50:51], v[54:55] offset0:160 offset1:176
	v_pk_mul_f32 v[50:51], v[16:17], v[46:47] op_sel:[1,1] op_sel_hi:[0,1] neg_lo:[0,1]
	v_pk_fma_f32 v[46:47], v[16:17], v[46:47], v[50:51] op_sel_hi:[1,0,1]
	s_nop 0
	v_pk_mul_f32 v[50:51], v[38:39], v[46:47] op_sel:[1,1] op_sel_hi:[1,0] neg_lo:[1,0]
	s_nop 0
	v_pk_fma_f32 v[38:39], v[38:39], v[46:47], v[50:51] op_sel_hi:[0,1,1]
	v_pk_mul_f32 v[50:51], v[16:17], v[46:47] op_sel:[1,1] op_sel_hi:[0,1] neg_lo:[0,1]
	v_pk_fma_f32 v[46:47], v[16:17], v[46:47], v[50:51] op_sel_hi:[1,0,1]
	s_nop 0
	v_pk_mul_f32 v[50:51], v[46:47], v[76:77] op_sel:[1,1] op_sel_hi:[0,1] neg_lo:[0,1]
	v_pk_fma_f32 v[50:51], v[46:47], v[76:77], v[50:51] op_sel_hi:[1,0,1]
	ds_write2_b64 v69, v[38:39], v[50:51] offset0:192 offset1:208
	v_pk_mul_f32 v[38:39], v[16:17], v[46:47] op_sel:[1,1] op_sel_hi:[0,1] neg_lo:[0,1]
	v_pk_fma_f32 v[38:39], v[16:17], v[46:47], v[38:39] op_sel_hi:[1,0,1]
	s_nop 0
	v_pk_mul_f32 v[46:47], v[42:43], v[38:39] op_sel:[1,1] op_sel_hi:[1,0] neg_lo:[1,0]
	s_nop 0
	v_pk_fma_f32 v[42:43], v[42:43], v[38:39], v[46:47] op_sel_hi:[0,1,1]
	v_pk_mul_f32 v[46:47], v[16:17], v[38:39] op_sel:[1,1] op_sel_hi:[0,1] neg_lo:[0,1]
	v_pk_fma_f32 v[38:39], v[16:17], v[38:39], v[46:47] op_sel_hi:[1,0,1]
	s_nop 0
	v_pk_mul_f32 v[46:47], v[38:39], v[84:85] op_sel:[1,1] op_sel_hi:[0,1] neg_lo:[0,1]
	v_pk_fma_f32 v[46:47], v[38:39], v[84:85], v[46:47] op_sel_hi:[1,0,1]
	ds_write2_b64 v68, v[42:43], v[46:47] offset0:224 offset1:240
	v_pk_mul_f32 v[42:43], v[16:17], v[38:39] op_sel:[1,1] op_sel_hi:[0,1] neg_lo:[0,1]
	v_pk_fma_f32 v[38:39], v[16:17], v[38:39], v[42:43] op_sel_hi:[1,0,1]
	s_nop 0
	v_pk_mul_f32 v[42:43], v[30:31], v[38:39] op_sel:[1,1] op_sel_hi:[1,0] neg_lo:[1,0]
	s_nop 0
	v_pk_fma_f32 v[30:31], v[30:31], v[38:39], v[42:43] op_sel_hi:[0,1,1]
	v_pk_mul_f32 v[42:43], v[16:17], v[38:39] op_sel:[1,1] op_sel_hi:[0,1] neg_lo:[0,1]
	v_pk_fma_f32 v[38:39], v[16:17], v[38:39], v[42:43] op_sel_hi:[1,0,1]
	s_nop 0
	v_pk_mul_f32 v[42:43], v[78:79], v[38:39] op_sel:[1,1] op_sel_hi:[1,0] neg_lo:[1,0]
	s_nop 0
	v_pk_fma_f32 v[42:43], v[78:79], v[38:39], v[42:43] op_sel_hi:[0,1,1]
	ds_write2_b64 v67, v[30:31], v[42:43] offset1:16
	v_pk_mul_f32 v[30:31], v[16:17], v[38:39] op_sel:[1,1] op_sel_hi:[0,1] neg_lo:[0,1]
	v_pk_fma_f32 v[30:31], v[16:17], v[38:39], v[30:31] op_sel_hi:[1,0,1]
	s_nop 0
	v_pk_mul_f32 v[38:39], v[34:35], v[30:31] op_sel:[1,1] op_sel_hi:[1,0] neg_lo:[1,0]
	s_nop 0
	v_pk_fma_f32 v[34:35], v[34:35], v[30:31], v[38:39] op_sel_hi:[0,1,1]
	v_pk_mul_f32 v[38:39], v[16:17], v[30:31] op_sel:[1,1] op_sel_hi:[0,1] neg_lo:[0,1]
	v_pk_fma_f32 v[30:31], v[16:17], v[30:31], v[38:39] op_sel_hi:[1,0,1]
	s_nop 0
	v_pk_mul_f32 v[38:39], v[52:53], v[30:31] op_sel:[1,1] op_sel_hi:[1,0] neg_lo:[1,0]
	s_nop 0
	v_pk_fma_f32 v[38:39], v[52:53], v[30:31], v[38:39] op_sel_hi:[0,1,1]
	ds_write2_b64 v66, v[34:35], v[38:39] offset0:32 offset1:48
	v_pk_mul_f32 v[34:35], v[16:17], v[30:31] op_sel:[1,1] op_sel_hi:[0,1] neg_lo:[0,1]
	v_pk_fma_f32 v[30:31], v[16:17], v[30:31], v[34:35] op_sel_hi:[1,0,1]
	s_nop 0
	v_pk_mul_f32 v[34:35], v[26:27], v[30:31] op_sel:[1,1] op_sel_hi:[1,0] neg_lo:[1,0]
	s_nop 0
	v_pk_fma_f32 v[26:27], v[26:27], v[30:31], v[34:35] op_sel_hi:[0,1,1]
	v_pk_mul_f32 v[34:35], v[16:17], v[30:31] op_sel:[1,1] op_sel_hi:[0,1] neg_lo:[0,1]
	v_pk_fma_f32 v[30:31], v[16:17], v[30:31], v[34:35] op_sel_hi:[1,0,1]
	s_nop 0
	v_pk_mul_f32 v[34:35], v[48:49], v[30:31] op_sel:[1,1] op_sel_hi:[1,0] neg_lo:[1,0]
	s_nop 0
	v_pk_fma_f32 v[34:35], v[48:49], v[30:31], v[34:35] op_sel_hi:[0,1,1]
	ds_write2_b64 v65, v[26:27], v[34:35] offset0:64 offset1:80
	v_pk_mul_f32 v[26:27], v[16:17], v[30:31] op_sel:[1,1] op_sel_hi:[0,1] neg_lo:[0,1]
	v_pk_fma_f32 v[26:27], v[16:17], v[30:31], v[26:27] op_sel_hi:[1,0,1]
	s_nop 0
	v_pk_mul_f32 v[30:31], v[28:29], v[26:27] op_sel:[1,1] op_sel_hi:[1,0] neg_lo:[1,0]
	s_nop 0
	v_pk_fma_f32 v[28:29], v[28:29], v[26:27], v[30:31] op_sel_hi:[0,1,1]
	v_pk_mul_f32 v[30:31], v[16:17], v[26:27] op_sel:[1,1] op_sel_hi:[0,1] neg_lo:[0,1]
	v_pk_fma_f32 v[26:27], v[16:17], v[26:27], v[30:31] op_sel_hi:[1,0,1]
	s_nop 0
	v_pk_mul_f32 v[30:31], v[80:81], v[26:27] op_sel:[1,1] op_sel_hi:[1,0] neg_lo:[1,0]
	s_nop 0
	v_pk_fma_f32 v[30:31], v[80:81], v[26:27], v[30:31] op_sel_hi:[0,1,1]
	ds_write2_b64 v64, v[28:29], v[30:31] offset0:96 offset1:112
	v_pk_mul_f32 v[28:29], v[16:17], v[26:27] op_sel:[1,1] op_sel_hi:[0,1] neg_lo:[0,1]
	v_pk_fma_f32 v[26:27], v[16:17], v[26:27], v[28:29] op_sel_hi:[1,0,1]
	s_nop 0
	v_pk_mul_f32 v[28:29], v[22:23], v[26:27] op_sel:[1,1] op_sel_hi:[1,0] neg_lo:[1,0]
	s_nop 0
	v_pk_fma_f32 v[22:23], v[22:23], v[26:27], v[28:29] op_sel_hi:[0,1,1]
	v_pk_mul_f32 v[28:29], v[16:17], v[26:27] op_sel:[1,1] op_sel_hi:[0,1] neg_lo:[0,1]
	v_pk_fma_f32 v[26:27], v[16:17], v[26:27], v[28:29] op_sel_hi:[1,0,1]
	s_nop 0
	v_pk_mul_f32 v[28:29], v[40:41], v[26:27] op_sel:[1,1] op_sel_hi:[1,0] neg_lo:[1,0]
	s_nop 0
	v_pk_fma_f32 v[28:29], v[40:41], v[26:27], v[28:29] op_sel_hi:[0,1,1]
	ds_write2_b64 v63, v[22:23], v[28:29] offset0:128 offset1:144
	v_pk_mul_f32 v[22:23], v[16:17], v[26:27] op_sel:[1,1] op_sel_hi:[0,1] neg_lo:[0,1]
	v_pk_fma_f32 v[22:23], v[16:17], v[26:27], v[22:23] op_sel_hi:[1,0,1]
	s_nop 0
	v_pk_mul_f32 v[26:27], v[24:25], v[22:23] op_sel:[1,1] op_sel_hi:[1,0] neg_lo:[1,0]
	s_nop 0
	v_pk_fma_f32 v[24:25], v[24:25], v[22:23], v[26:27] op_sel_hi:[0,1,1]
	v_pk_mul_f32 v[26:27], v[16:17], v[22:23] op_sel:[1,1] op_sel_hi:[0,1] neg_lo:[0,1]
	v_pk_fma_f32 v[22:23], v[16:17], v[22:23], v[26:27] op_sel_hi:[1,0,1]
	s_nop 0
	v_pk_mul_f32 v[26:27], v[44:45], v[22:23] op_sel:[1,1] op_sel_hi:[1,0] neg_lo:[1,0]
	s_nop 0
	v_pk_fma_f32 v[26:27], v[44:45], v[22:23], v[26:27] op_sel_hi:[0,1,1]
	ds_write2_b64 v62, v[24:25], v[26:27] offset0:160 offset1:176
	v_pk_mul_f32 v[24:25], v[16:17], v[22:23] op_sel:[1,1] op_sel_hi:[0,1] neg_lo:[0,1]
	v_pk_fma_f32 v[22:23], v[16:17], v[22:23], v[24:25] op_sel_hi:[1,0,1]
	s_nop 0
	v_pk_mul_f32 v[24:25], v[18:19], v[22:23] op_sel:[1,1] op_sel_hi:[1,0] neg_lo:[1,0]
	s_nop 0
	v_pk_fma_f32 v[18:19], v[18:19], v[22:23], v[24:25] op_sel_hi:[0,1,1]
	v_pk_mul_f32 v[24:25], v[16:17], v[22:23] op_sel:[1,1] op_sel_hi:[0,1] neg_lo:[0,1]
	v_pk_fma_f32 v[22:23], v[16:17], v[22:23], v[24:25] op_sel_hi:[1,0,1]
	s_nop 0
	v_pk_mul_f32 v[24:25], v[32:33], v[22:23] op_sel:[1,1] op_sel_hi:[1,0] neg_lo:[1,0]
	s_nop 0
	v_pk_fma_f32 v[24:25], v[32:33], v[22:23], v[24:25] op_sel_hi:[0,1,1]
	ds_write2_b64 v15, v[18:19], v[24:25] offset0:192 offset1:208
	v_pk_mul_f32 v[18:19], v[16:17], v[22:23] op_sel:[1,1] op_sel_hi:[0,1] neg_lo:[0,1]
	v_pk_fma_f32 v[18:19], v[16:17], v[22:23], v[18:19] op_sel_hi:[1,0,1]
	s_nop 0
	v_pk_mul_f32 v[22:23], v[20:21], v[18:19] op_sel:[1,1] op_sel_hi:[1,0] neg_lo:[1,0]
	s_nop 0
	v_pk_fma_f32 v[20:21], v[20:21], v[18:19], v[22:23] op_sel_hi:[0,1,1]
	v_pk_mul_f32 v[22:23], v[16:17], v[18:19] op_sel:[1,1] op_sel_hi:[0,1] neg_lo:[0,1]
	v_pk_fma_f32 v[16:17], v[16:17], v[18:19], v[22:23] op_sel_hi:[1,0,1]
	s_nop 0
	v_pk_mul_f32 v[18:19], v[36:37], v[16:17] op_sel:[1,1] op_sel_hi:[1,0] neg_lo:[1,0]
	s_nop 0
	v_pk_fma_f32 v[16:17], v[36:37], v[16:17], v[18:19] op_sel_hi:[0,1,1]
	ds_write2_b64 v13, v[20:21], v[16:17] offset0:224 offset1:240
	v_mov_b32_e32 v16, v182
	v_mov_b32_e32 v10, v176
	v_mov_b32_e32 v17, v175
	s_waitcnt lgkmcnt(0)
	s_barrier
	v_lshlrev_b32_e32 v190, 3, v16
	v_add_u32_e32 v190, 0x1000, v190
	global_load_dwordx2 v[202:203], v190, s[46:47] offset:-4096
	global_load_dwordx2 v[204:205], v190, s[46:47]
	v_add_u32_e32 v190, 0x2000, v190
	global_load_dwordx2 v[206:207], v190, s[46:47] offset:-4096
	global_load_dwordx2 v[208:209], v190, s[46:47]
	v_add_u32_e32 v190, 0x2000, v190
	global_load_dwordx2 v[210:211], v190, s[46:47] offset:-4096
	global_load_dwordx2 v[212:213], v190, s[46:47]
	v_add_u32_e32 v190, 0x2000, v190
	global_load_dwordx2 v[214:215], v190, s[46:47] offset:-4096
	global_load_dwordx2 v[216:217], v190, s[46:47]
	v_add_u32_e32 v190, 0x2000, v190
	global_load_dwordx2 v[218:219], v190, s[46:47] offset:-4096
	global_load_dwordx2 v[220:221], v190, s[46:47]
	v_add_u32_e32 v190, 0x2000, v190
	global_load_dwordx2 v[222:223], v190, s[46:47] offset:-4096
	global_load_dwordx2 v[224:225], v190, s[46:47]
	v_add_u32_e32 v190, 0x2000, v190
	global_load_dwordx2 v[226:227], v190, s[46:47] offset:-4096
	global_load_dwordx2 v[228:229], v190, s[46:47]
	v_add_u32_e32 v190, 0x2000, v190
	global_load_dwordx2 v[230:231], v190, s[46:47] offset:-4096
	global_load_dwordx2 v[232:233], v190, s[46:47]
	v_mov_b32_e32 v50, v165
	v_lshlrev_b32_e32 v13, 3, v17
	v_lshlrev_b32_e32 v48, 3, v10
	v_add3_u32 v10, 0, v13, v48
	v_xor_b32_e32 v13, 1, v17
	v_xor_b32_e32 v34, 8, v17
	v_xor_b32_e32 v36, 9, v17
	v_lshlrev_b32_e32 v13, 3, v13
	v_xor_b32_e32 v15, 2, v17
	v_xor_b32_e32 v24, 3, v17
	v_xor_b32_e32 v26, 4, v17
	v_xor_b32_e32 v28, 5, v17
	v_xor_b32_e32 v30, 6, v17
	v_xor_b32_e32 v32, 7, v17
	v_lshlrev_b32_e32 v34, 3, v34
	v_lshlrev_b32_e32 v36, 3, v36
	v_xor_b32_e32 v38, 10, v17
	v_xor_b32_e32 v40, 11, v17
	v_xor_b32_e32 v42, 12, v17
	v_xor_b32_e32 v44, 13, v17
	v_xor_b32_e32 v46, 14, v17
	v_xor_b32_e32 v17, 15, v17
	v_add3_u32 v13, 0, v13, v48
	v_lshlrev_b32_e32 v15, 3, v15
	v_lshlrev_b32_e32 v24, 3, v24
	v_lshlrev_b32_e32 v26, 3, v26
	v_lshlrev_b32_e32 v28, 3, v28
	v_lshlrev_b32_e32 v30, 3, v30
	v_lshlrev_b32_e32 v32, 3, v32
	v_add3_u32 v57, 0, v34, v48
	v_add3_u32 v58, 0, v36, v48
	v_lshlrev_b32_e32 v38, 3, v38
	v_lshlrev_b32_e32 v40, 3, v40
	v_lshlrev_b32_e32 v42, 3, v42
	v_lshlrev_b32_e32 v44, 3, v44
	v_lshlrev_b32_e32 v46, 3, v46
	v_lshlrev_b32_e32 v17, 3, v17
	ds_read_b64 v[18:19], v10
	ds_read_b64 v[20:21], v13
	v_add3_u32 v15, 0, v15, v48
	v_add3_u32 v52, 0, v24, v48
	v_add3_u32 v53, 0, v26, v48
	v_add3_u32 v54, 0, v28, v48
	v_add3_u32 v55, 0, v30, v48
	v_add3_u32 v56, 0, v32, v48
	ds_read_b64 v[34:35], v57
	ds_read_b64 v[36:37], v58
	v_add3_u32 v59, 0, v38, v48
	v_add3_u32 v60, 0, v40, v48
	v_add3_u32 v61, 0, v42, v48
	v_add3_u32 v62, 0, v44, v48
	v_add3_u32 v63, 0, v46, v48
	v_add3_u32 v64, 0, v17, v48
	ds_read_b64 v[22:23], v15
	ds_read_b64 v[24:25], v52
	ds_read_b64 v[26:27], v53
	ds_read_b64 v[28:29], v54
	ds_read_b64 v[30:31], v55
	ds_read_b64 v[32:33], v56
	ds_read_b64 v[38:39], v59
	ds_read_b64 v[40:41], v60
	ds_read_b64 v[42:43], v61
	ds_read_b64 v[44:45], v62
	ds_read_b64 v[46:47], v63
	ds_read_b64 v[48:49], v64
	s_waitcnt lgkmcnt(13)
	v_pk_add_f32 v[70:71], v[18:19], v[34:35]
	v_pk_add_f32 v[18:19], v[18:19], v[34:35] neg_lo:[0,1] neg_hi:[0,1]
	s_waitcnt lgkmcnt(12)
	v_pk_add_f32 v[34:35], v[20:21], v[36:37]
	v_pk_add_f32 v[20:21], v[20:21], v[36:37] neg_lo:[0,1] neg_hi:[0,1]
	v_mov_b32_e32 v66, v167
	v_mov_b32_e32 v68, v169
	s_nop 0
	v_pk_mul_f32 v[36:37], v[20:21], v[68:69] op_sel:[1,0] op_sel_hi:[0,0] neg_lo:[1,1] neg_hi:[0,1]
	v_pk_fma_f32 v[20:21], v[20:21], v[50:51], v[36:37] op_sel_hi:[1,0,1]
	s_waitcnt lgkmcnt(5)
	v_pk_add_f32 v[36:37], v[22:23], v[38:39]
	v_pk_add_f32 v[22:23], v[22:23], v[38:39] neg_lo:[0,1] neg_hi:[0,1]
	s_nop 0
	v_pk_mul_f32 v[38:39], v[22:23], v[66:67] op_sel:[1,0] op_sel_hi:[0,0] neg_lo:[1,1] neg_hi:[0,1]
	v_pk_fma_f32 v[22:23], v[22:23], v[66:67], v[38:39] op_sel_hi:[1,0,1]
	s_waitcnt lgkmcnt(4)
	v_pk_add_f32 v[38:39], v[24:25], v[40:41]
	v_pk_add_f32 v[24:25], v[24:25], v[40:41] neg_lo:[0,1] neg_hi:[0,1]
	s_nop 0
	v_pk_mul_f32 v[40:41], v[24:25], v[68:69] op_sel_hi:[1,0]
	s_nop 0
	v_pk_fma_f32 v[24:25], v[24:25], v[50:51], v[40:41] op_sel:[1,0,0] op_sel_hi:[0,0,1] neg_lo:[1,1,0] neg_hi:[0,1,0]
	s_waitcnt lgkmcnt(3)
	v_pk_add_f32 v[40:41], v[26:27], v[42:43]
	v_pk_add_f32 v[26:27], v[26:27], v[42:43] neg_lo:[0,1] neg_hi:[0,1]
	v_xor_b32_e32 v73, 0x80000000, v26
	v_mov_b32_e32 v72, v27
	s_waitcnt lgkmcnt(2)
	v_pk_add_f32 v[26:27], v[28:29], v[44:45]
	v_pk_add_f32 v[28:29], v[28:29], v[44:45] neg_lo:[0,1] neg_hi:[0,1]
	s_nop 0
	v_pk_mul_f32 v[42:43], v[28:29], v[68:69] op_sel_hi:[1,0] neg_lo:[0,1] neg_hi:[0,1]
	s_nop 0
	v_pk_fma_f32 v[28:29], v[28:29], v[50:51], v[42:43] op_sel:[1,0,0] op_sel_hi:[0,0,1] neg_lo:[1,1,0] neg_hi:[0,1,0]
	s_waitcnt lgkmcnt(1)
	v_pk_add_f32 v[42:43], v[30:31], v[46:47]
	v_pk_add_f32 v[30:31], v[30:31], v[46:47] neg_lo:[0,1] neg_hi:[0,1]
	s_nop 0
	v_pk_mul_f32 v[44:45], v[30:31], v[66:67] op_sel:[1,0] op_sel_hi:[0,0] neg_lo:[1,1] neg_hi:[0,1]
	s_nop 0
	v_pk_fma_f32 v[30:31], v[30:31], v[66:67], v[44:45] op_sel_hi:[1,0,1] neg_lo:[0,1,0] neg_hi:[0,1,0]
	s_waitcnt lgkmcnt(0)
	v_pk_add_f32 v[44:45], v[32:33], v[48:49]
	v_pk_add_f32 v[32:33], v[32:33], v[48:49] neg_lo:[0,1] neg_hi:[0,1]
	v_pk_add_f32 v[48:49], v[34:35], v[26:27]
	v_pk_add_f32 v[26:27], v[34:35], v[26:27] neg_lo:[0,1] neg_hi:[0,1]
	s_nop 0
	v_pk_mul_f32 v[34:35], v[26:27], v[66:67] op_sel:[1,0] op_sel_hi:[0,0] neg_lo:[1,1] neg_hi:[0,1]
	v_pk_fma_f32 v[26:27], v[26:27], v[66:67], v[34:35] op_sel_hi:[1,0,1]
	v_pk_add_f32 v[34:35], v[36:37], v[42:43]
	v_pk_add_f32 v[36:37], v[36:37], v[42:43] neg_lo:[0,1] neg_hi:[0,1]
	v_pk_mul_f32 v[46:47], v[32:33], v[68:69] op_sel:[1,0] op_sel_hi:[0,0] neg_lo:[1,1] neg_hi:[0,1]
	v_xor_b32_e32 v43, 0x80000000, v36
	v_mov_b32_e32 v42, v37
	v_pk_add_f32 v[36:37], v[38:39], v[44:45]
	v_pk_add_f32 v[38:39], v[38:39], v[44:45] neg_lo:[0,1] neg_hi:[0,1]
	v_pk_fma_f32 v[46:47], v[32:33], v[50:51], v[46:47] op_sel_hi:[1,0,1] neg_lo:[0,1,0] neg_hi:[0,1,0]
	v_pk_add_f32 v[32:33], v[70:71], v[40:41]
	v_pk_mul_f32 v[44:45], v[38:39], v[66:67] op_sel:[1,0] op_sel_hi:[0,0] neg_lo:[1,1] neg_hi:[0,1]
	v_pk_add_f32 v[40:41], v[70:71], v[40:41] neg_lo:[0,1] neg_hi:[0,1]
	v_pk_fma_f32 v[38:39], v[38:39], v[66:67], v[44:45] op_sel_hi:[1,0,1] neg_lo:[0,1,0] neg_hi:[0,1,0]
	v_pk_add_f32 v[44:45], v[32:33], v[34:35]
	v_pk_add_f32 v[32:33], v[32:33], v[34:35] neg_lo:[0,1] neg_hi:[0,1]
	v_pk_add_f32 v[34:35], v[48:49], v[36:37]
	v_pk_add_f32 v[36:37], v[48:49], v[36:37] neg_lo:[0,1] neg_hi:[0,1]
	v_pk_add_f32 v[50:51], v[44:45], v[34:35]
	v_xor_b32_e32 v49, 0x80000000, v36
	v_mov_b32_e32 v48, v37
	v_pk_add_f32 v[36:37], v[44:45], v[34:35] neg_lo:[0,1] neg_hi:[0,1]
	v_pk_add_f32 v[68:69], v[32:33], v[48:49]
	v_pk_add_f32 v[44:45], v[32:33], v[48:49] neg_lo:[0,1] neg_hi:[0,1]
	v_pk_add_f32 v[32:33], v[40:41], v[42:43]
	v_pk_add_f32 v[34:35], v[40:41], v[42:43] neg_lo:[0,1] neg_hi:[0,1]
	v_pk_add_f32 v[40:41], v[26:27], v[38:39]
	v_pk_add_f32 v[26:27], v[26:27], v[38:39] neg_lo:[0,1] neg_hi:[0,1]
	v_pk_add_f32 v[42:43], v[32:33], v[40:41] neg_lo:[0,1] neg_hi:[0,1]
	v_xor_b32_e32 v39, 0x80000000, v26
	v_mov_b32_e32 v38, v27
	v_pk_add_f32 v[26:27], v[32:33], v[40:41]
	v_pk_add_f32 v[40:41], v[20:21], v[28:29]
	v_pk_add_f32 v[20:21], v[20:21], v[28:29] neg_lo:[0,1] neg_hi:[0,1]
	v_pk_add_f32 v[32:33], v[34:35], v[38:39]
	v_pk_mul_f32 v[28:29], v[66:67], v[20:21] op_sel:[0,1] op_sel_hi:[0,0] neg_lo:[1,1] neg_hi:[1,0]
	v_pk_fma_f32 v[20:21], v[66:67], v[20:21], v[28:29] op_sel_hi:[0,1,1]
	v_pk_add_f32 v[28:29], v[22:23], v[30:31]
	v_pk_add_f32 v[22:23], v[22:23], v[30:31] neg_lo:[0,1] neg_hi:[0,1]
	v_pk_add_f32 v[38:39], v[34:35], v[38:39] neg_lo:[0,1] neg_hi:[0,1]
	v_xor_b32_e32 v31, 0x80000000, v22
	v_mov_b32_e32 v30, v23
	v_pk_add_f32 v[22:23], v[24:25], v[46:47]
	v_pk_add_f32 v[24:25], v[24:25], v[46:47] neg_lo:[0,1] neg_hi:[0,1]
	v_pk_add_f32 v[34:35], v[18:19], v[72:73]
	v_pk_mul_f32 v[46:47], v[66:67], v[24:25] op_sel:[0,1] op_sel_hi:[0,0] neg_lo:[1,1] neg_hi:[1,0]
	v_pk_fma_f32 v[24:25], v[66:67], v[24:25], v[46:47] op_sel_hi:[0,1,1] neg_lo:[1,0,0] neg_hi:[1,0,0]
	v_pk_add_f32 v[46:47], v[34:35], v[28:29]
	v_pk_add_f32 v[28:29], v[34:35], v[28:29] neg_lo:[0,1] neg_hi:[0,1]
	v_pk_add_f32 v[34:35], v[40:41], v[22:23]
	v_pk_add_f32 v[22:23], v[40:41], v[22:23] neg_lo:[0,1] neg_hi:[0,1]
	v_pk_add_f32 v[18:19], v[18:19], v[72:73] neg_lo:[0,1] neg_hi:[0,1]
	v_pk_add_f32 v[66:67], v[28:29], v[22:23] op_sel:[0,1] op_sel_hi:[1,0] neg_hi:[0,1]
	v_pk_add_f32 v[48:49], v[28:29], v[22:23] op_sel:[0,1] op_sel_hi:[1,0] neg_lo:[0,1]
	v_pk_add_f32 v[28:29], v[18:19], v[30:31]
	v_pk_add_f32 v[18:19], v[18:19], v[30:31] neg_lo:[0,1] neg_hi:[0,1]
	v_pk_add_f32 v[30:31], v[20:21], v[24:25]
	v_pk_add_f32 v[20:21], v[20:21], v[24:25] neg_lo:[0,1] neg_hi:[0,1]
	v_pk_add_f32 v[22:23], v[46:47], v[34:35]
	v_xor_b32_e32 v25, 0x80000000, v20
	v_mov_b32_e32 v24, v21
	s_waitcnt vmcnt(0)
	v_pk_add_f32 v[40:41], v[46:47], v[34:35] neg_lo:[0,1] neg_hi:[0,1]
	v_pk_add_f32 v[34:35], v[18:19], v[24:25]
	v_pk_add_f32 v[18:19], v[18:19], v[24:25] neg_lo:[0,1] neg_hi:[0,1]
	v_pk_add_f32 v[70:71], v[28:29], v[30:31]
	v_pk_add_f32 v[46:47], v[28:29], v[30:31] neg_lo:[0,1] neg_hi:[0,1]
	s_nop 0
	v_pk_mul_f32 v[24:25], v[50:51], v[202:203] op_sel:[1,1] op_sel_hi:[1,0] neg_lo:[1,0]
	s_nop 0
	v_pk_fma_f32 v[20:21], v[50:51], v[202:203], v[24:25] op_sel_hi:[0,1,1]
	s_nop 0
	v_pk_mul_f32 v[28:29], v[204:205], v[22:23] op_sel:[1,1] op_sel_hi:[0,1] neg_lo:[0,1]
	v_pk_fma_f32 v[22:23], v[204:205], v[22:23], v[28:29] op_sel_hi:[1,0,1]
	s_nop 0
	v_pk_mul_f32 v[28:29], v[26:27], v[206:207] op_sel:[1,1] op_sel_hi:[1,0] neg_lo:[1,0]
	s_nop 0
	v_pk_fma_f32 v[24:25], v[26:27], v[206:207], v[28:29] op_sel_hi:[0,1,1]
	s_nop 0
	v_pk_mul_f32 v[28:29], v[208:209], v[70:71] op_sel:[1,1] op_sel_hi:[0,1] neg_lo:[0,1]
	v_pk_fma_f32 v[26:27], v[208:209], v[70:71], v[28:29] op_sel_hi:[1,0,1]
	s_nop 0
	v_pk_mul_f32 v[30:31], v[68:69], v[210:211] op_sel:[1,1] op_sel_hi:[1,0] neg_lo:[1,0]
	s_nop 0
	v_pk_fma_f32 v[28:29], v[68:69], v[210:211], v[30:31] op_sel_hi:[0,1,1]
	v_mov_b32_e32 v68, v169
	s_nop 0
	v_pk_mul_f32 v[50:51], v[212:213], v[66:67] op_sel:[1,1] op_sel_hi:[0,1] neg_lo:[0,1]
	v_pk_fma_f32 v[30:31], v[212:213], v[66:67], v[50:51] op_sel_hi:[1,0,1]
	s_nop 0
	v_pk_mul_f32 v[66:67], v[32:33], v[214:215] op_sel:[1,1] op_sel_hi:[1,0] neg_lo:[1,0]
	s_nop 0
	v_pk_fma_f32 v[32:33], v[32:33], v[214:215], v[66:67] op_sel_hi:[0,1,1]
	s_nop 0
	v_pk_mul_f32 v[66:67], v[216:217], v[34:35] op_sel:[1,1] op_sel_hi:[0,1] neg_lo:[0,1]
	v_pk_fma_f32 v[34:35], v[216:217], v[34:35], v[66:67] op_sel_hi:[1,0,1]
	s_nop 0
	v_pk_mul_f32 v[66:67], v[36:37], v[218:219] op_sel:[1,1] op_sel_hi:[1,0] neg_lo:[1,0]
	s_nop 0
	v_pk_fma_f32 v[36:37], v[36:37], v[218:219], v[66:67] op_sel_hi:[0,1,1]
	v_pk_add_f32 v[70:71], v[20:21], v[36:37]
	v_pk_add_f32 v[20:21], v[20:21], v[36:37] neg_lo:[0,1] neg_hi:[0,1]
	s_nop 0
	v_pk_mul_f32 v[66:67], v[40:41], v[220:221] op_sel:[1,1] op_sel_hi:[1,0] neg_lo:[1,0]
	s_nop 0
	v_pk_fma_f32 v[40:41], v[40:41], v[220:221], v[66:67] op_sel_hi:[0,1,1]
	v_pk_add_f32 v[36:37], v[22:23], v[40:41]
	v_pk_add_f32 v[22:23], v[22:23], v[40:41] neg_lo:[0,1] neg_hi:[0,1]
	s_nop 0
	v_pk_mul_f32 v[66:67], v[42:43], v[222:223] op_sel:[1,1] op_sel_hi:[1,0] neg_lo:[1,0]
	s_nop 0
	v_pk_fma_f32 v[42:43], v[42:43], v[222:223], v[66:67] op_sel_hi:[0,1,1]
	s_nop 0
	v_pk_mul_f32 v[66:67], v[46:47], v[224:225] op_sel:[1,1] op_sel_hi:[1,0] neg_lo:[1,0]
	s_nop 0
	v_pk_fma_f32 v[46:47], v[46:47], v[224:225], v[66:67] op_sel_hi:[0,1,1]
	s_nop 0
	v_pk_mul_f32 v[66:67], v[44:45], v[226:227] op_sel:[1,1] op_sel_hi:[1,0] neg_lo:[1,0]
	s_nop 0
	v_pk_fma_f32 v[44:45], v[44:45], v[226:227], v[66:67] op_sel_hi:[0,1,1]
	s_nop 0
	v_pk_mul_f32 v[66:67], v[48:49], v[228:229] op_sel:[1,1] op_sel_hi:[1,0] neg_lo:[1,0]
	s_nop 0
	v_pk_fma_f32 v[48:49], v[48:49], v[228:229], v[66:67] op_sel_hi:[0,1,1]
	s_nop 0
	v_pk_mul_f32 v[66:67], v[38:39], v[230:231] op_sel:[1,1] op_sel_hi:[1,0] neg_lo:[1,0]
	s_nop 0
	v_pk_fma_f32 v[38:39], v[38:39], v[230:231], v[66:67] op_sel_hi:[0,1,1]
	v_mov_b32_e32 v50, v232
	v_mov_b32_e32 v51, v233
	v_lshlrev_b32_e32 v190, 3, v16
	v_add_u32_e32 v190, 0x11000, v190
	global_load_dwordx2 v[202:203], v190, s[46:47] offset:-4096
	global_load_dwordx2 v[204:205], v190, s[46:47]
	v_add_u32_e32 v190, 0x2000, v190
	global_load_dwordx2 v[206:207], v190, s[46:47] offset:-4096
	global_load_dwordx2 v[208:209], v190, s[46:47]
	v_add_u32_e32 v190, 0x2000, v190
	global_load_dwordx2 v[210:211], v190, s[46:47] offset:-4096
	global_load_dwordx2 v[212:213], v190, s[46:47]
	v_add_u32_e32 v190, 0x2000, v190
	global_load_dwordx2 v[214:215], v190, s[46:47] offset:-4096
	global_load_dwordx2 v[216:217], v190, s[46:47]
	v_add_u32_e32 v190, 0x2000, v190
	global_load_dwordx2 v[218:219], v190, s[46:47] offset:-4096
	global_load_dwordx2 v[220:221], v190, s[46:47]
	v_add_u32_e32 v190, 0x2000, v190
	global_load_dwordx2 v[222:223], v190, s[46:47] offset:-4096
	global_load_dwordx2 v[224:225], v190, s[46:47]
	v_add_u32_e32 v190, 0x2000, v190
	global_load_dwordx2 v[226:227], v190, s[46:47] offset:-4096
	global_load_dwordx2 v[228:229], v190, s[46:47]
	v_add_u32_e32 v190, 0x2000, v190
	global_load_dwordx2 v[230:231], v190, s[46:47] offset:-4096
	global_load_dwordx2 v[232:233], v190, s[46:47]
	s_nop 0
	v_pk_mul_f32 v[66:67], v[18:19], v[50:51] op_sel:[1,1] op_sel_hi:[1,0] neg_lo:[1,0]
	s_nop 0
	v_pk_fma_f32 v[18:19], v[18:19], v[50:51], v[66:67] op_sel_hi:[0,1,1]
	v_mov_b32_e32 v50, v165
	v_mov_b32_e32 v66, v167
	s_nop 0
	v_pk_mul_f32 v[40:41], v[22:23], v[68:69] op_sel:[1,0] op_sel_hi:[0,0] neg_lo:[1,0]
	v_pk_fma_f32 v[22:23], v[22:23], v[50:51], v[40:41] op_sel_hi:[1,0,1]
	v_pk_add_f32 v[40:41], v[24:25], v[42:43]
	v_pk_add_f32 v[24:25], v[24:25], v[42:43] neg_lo:[0,1] neg_hi:[0,1]
	s_nop 0
	v_pk_mul_f32 v[42:43], v[24:25], v[66:67] op_sel:[1,0] op_sel_hi:[0,0] neg_lo:[1,0]
	v_pk_fma_f32 v[24:25], v[24:25], v[66:67], v[42:43] op_sel_hi:[1,0,1]
	v_pk_add_f32 v[42:43], v[26:27], v[46:47]
	v_pk_add_f32 v[26:27], v[26:27], v[46:47] neg_lo:[0,1] neg_hi:[0,1]
	s_nop 0
	v_pk_mul_f32 v[46:47], v[26:27], v[68:69] op_sel_hi:[1,0]
	s_nop 0
	v_pk_fma_f32 v[26:27], v[26:27], v[50:51], v[46:47] op_sel:[1,0,0] op_sel_hi:[0,0,1] neg_lo:[1,0,0]
	v_pk_add_f32 v[46:47], v[28:29], v[44:45]
	v_pk_add_f32 v[28:29], v[28:29], v[44:45] neg_lo:[0,1] neg_hi:[0,1]
	v_mov_b32_e32 v17, v175
	v_xor_b32_e32 v44, 0x80000000, v29
	v_mov_b32_e32 v45, v28
	v_pk_add_f32 v[28:29], v[30:31], v[48:49]
	v_pk_add_f32 v[30:31], v[30:31], v[48:49] neg_lo:[0,1] neg_hi:[0,1]
	s_nop 0
	v_pk_mul_f32 v[48:49], v[30:31], v[68:69] op_sel_hi:[1,0] neg_lo:[0,1] neg_hi:[0,1]
	s_nop 0
	v_pk_fma_f32 v[30:31], v[30:31], v[50:51], v[48:49] op_sel:[1,0,0] op_sel_hi:[0,0,1] neg_lo:[1,0,0]
	v_pk_add_f32 v[48:49], v[32:33], v[38:39]
	v_pk_add_f32 v[32:33], v[32:33], v[38:39] neg_lo:[0,1] neg_hi:[0,1]
	s_nop 0
	v_pk_mul_f32 v[38:39], v[32:33], v[66:67] op_sel:[1,0] op_sel_hi:[0,0] neg_lo:[1,0]
	s_nop 0
	v_pk_fma_f32 v[32:33], v[32:33], v[66:67], v[38:39] op_sel_hi:[1,0,1] neg_lo:[0,1,0] neg_hi:[0,1,0]
	v_pk_add_f32 v[38:39], v[34:35], v[18:19]
	v_pk_add_f32 v[18:19], v[34:35], v[18:19] neg_lo:[0,1] neg_hi:[0,1]
	s_nop 0
	v_pk_mul_f32 v[34:35], v[18:19], v[68:69] op_sel:[1,0] op_sel_hi:[0,0] neg_lo:[1,0]
	v_mov_b32_e32 v68, v169
	v_pk_fma_f32 v[18:19], v[18:19], v[50:51], v[34:35] op_sel_hi:[1,0,1] neg_lo:[0,1,0] neg_hi:[0,1,0]
	v_pk_add_f32 v[50:51], v[36:37], v[28:29]
	v_pk_add_f32 v[28:29], v[36:37], v[28:29] neg_lo:[0,1] neg_hi:[0,1]
	v_pk_add_f32 v[34:35], v[70:71], v[46:47]
	v_pk_mul_f32 v[36:37], v[28:29], v[66:67] op_sel:[1,0] op_sel_hi:[0,0] neg_lo:[1,0]
	v_pk_add_f32 v[46:47], v[70:71], v[46:47] neg_lo:[0,1] neg_hi:[0,1]
	v_pk_fma_f32 v[28:29], v[28:29], v[66:67], v[36:37] op_sel_hi:[1,0,1]
	v_pk_add_f32 v[36:37], v[40:41], v[48:49]
	v_pk_add_f32 v[40:41], v[40:41], v[48:49] neg_lo:[0,1] neg_hi:[0,1]
	s_nop 0
	v_xor_b32_e32 v48, 0x80000000, v41
	v_mov_b32_e32 v49, v40
	v_pk_add_f32 v[40:41], v[42:43], v[38:39]
	v_pk_add_f32 v[38:39], v[42:43], v[38:39] neg_lo:[0,1] neg_hi:[0,1]
	s_nop 0
	v_pk_mul_f32 v[42:43], v[66:67], v[38:39] op_sel:[0,1] op_sel_hi:[0,0] neg_lo:[0,1]
	v_pk_fma_f32 v[38:39], v[38:39], v[66:67], v[42:43] op_sel_hi:[1,0,1] neg_lo:[0,1,0] neg_hi:[0,1,0]
	v_pk_add_f32 v[42:43], v[34:35], v[36:37]
	v_pk_add_f32 v[34:35], v[34:35], v[36:37] neg_lo:[0,1] neg_hi:[0,1]
	v_pk_add_f32 v[36:37], v[50:51], v[40:41]
	v_pk_add_f32 v[40:41], v[50:51], v[40:41] neg_lo:[0,1] neg_hi:[0,1]
	s_nop 0
	v_xor_b32_e32 v50, 0x80000000, v41
	v_mov_b32_e32 v51, v40
	v_pk_add_f32 v[40:41], v[42:43], v[36:37]
	v_pk_add_f32 v[36:37], v[42:43], v[36:37] neg_lo:[0,1] neg_hi:[0,1]
	v_pk_add_f32 v[42:43], v[34:35], v[50:51]
	v_pk_add_f32 v[34:35], v[34:35], v[50:51] neg_lo:[0,1] neg_hi:[0,1]
	v_pk_add_f32 v[50:51], v[46:47], v[48:49]
	v_pk_add_f32 v[46:47], v[46:47], v[48:49] neg_lo:[0,1] neg_hi:[0,1]
	v_pk_add_f32 v[48:49], v[28:29], v[38:39]
	v_pk_add_f32 v[28:29], v[28:29], v[38:39] neg_lo:[0,1] neg_hi:[0,1]
	s_nop 0
	v_xor_b32_e32 v38, 0x80000000, v29
	v_mov_b32_e32 v39, v28
	v_pk_add_f32 v[28:29], v[50:51], v[48:49]
	v_pk_add_f32 v[48:49], v[50:51], v[48:49] neg_lo:[0,1] neg_hi:[0,1]
	v_pk_add_f32 v[50:51], v[46:47], v[38:39]
	v_pk_add_f32 v[38:39], v[46:47], v[38:39] neg_lo:[0,1] neg_hi:[0,1]
	v_pk_add_f32 v[46:47], v[20:21], v[44:45]
	v_pk_add_f32 v[20:21], v[20:21], v[44:45] neg_lo:[0,1] neg_hi:[0,1]
	v_pk_add_f32 v[44:45], v[22:23], v[30:31]
	v_pk_add_f32 v[22:23], v[22:23], v[30:31] neg_lo:[0,1] neg_hi:[0,1]
	s_nop 0
	v_pk_mul_f32 v[30:31], v[66:67], v[22:23] op_sel:[0,1] op_sel_hi:[0,0] neg_lo:[0,1]
	v_pk_fma_f32 v[22:23], v[66:67], v[22:23], v[30:31] op_sel_hi:[0,1,1]
	v_pk_add_f32 v[30:31], v[24:25], v[32:33]
	v_pk_add_f32 v[24:25], v[24:25], v[32:33] neg_lo:[0,1] neg_hi:[0,1]
	s_nop 0
	v_xor_b32_e32 v32, 0x80000000, v25
	v_mov_b32_e32 v33, v24
	v_pk_add_f32 v[24:25], v[26:27], v[18:19]
	v_pk_add_f32 v[18:19], v[26:27], v[18:19] neg_lo:[0,1] neg_hi:[0,1]
	s_nop 0
	v_pk_mul_f32 v[26:27], v[66:67], v[18:19] op_sel:[0,1] op_sel_hi:[0,0] neg_lo:[0,1]
	v_pk_fma_f32 v[18:19], v[66:67], v[18:19], v[26:27] op_sel_hi:[0,1,1] neg_lo:[1,0,0] neg_hi:[1,0,0]
	v_pk_add_f32 v[26:27], v[46:47], v[30:31]
	v_pk_add_f32 v[30:31], v[46:47], v[30:31] neg_lo:[0,1] neg_hi:[0,1]
	v_pk_add_f32 v[46:47], v[44:45], v[24:25]
	v_pk_add_f32 v[24:25], v[44:45], v[24:25] neg_lo:[0,1] neg_hi:[0,1]
	v_mov_b32_e32 v66, v167
	v_xor_b32_e32 v44, 0x80000000, v25
	v_mov_b32_e32 v45, v24
	v_pk_add_f32 v[24:25], v[26:27], v[46:47]
	v_pk_add_f32 v[26:27], v[26:27], v[46:47] neg_lo:[0,1] neg_hi:[0,1]
	v_pk_add_f32 v[46:47], v[30:31], v[44:45]
	v_pk_add_f32 v[30:31], v[30:31], v[44:45] neg_lo:[0,1] neg_hi:[0,1]
	v_pk_add_f32 v[44:45], v[20:21], v[32:33]
	v_pk_add_f32 v[20:21], v[20:21], v[32:33] neg_lo:[0,1] neg_hi:[0,1]
	v_pk_add_f32 v[32:33], v[22:23], v[18:19]
	v_pk_add_f32 v[18:19], v[22:23], v[18:19] neg_lo:[0,1] neg_hi:[0,1]
	s_nop 0
	v_xor_b32_e32 v22, 0x80000000, v19
	v_mov_b32_e32 v23, v18
	v_pk_add_f32 v[18:19], v[44:45], v[32:33]
	v_pk_add_f32 v[32:33], v[44:45], v[32:33] neg_lo:[0,1] neg_hi:[0,1]
	v_pk_add_f32 v[44:45], v[20:21], v[22:23]
	v_pk_add_f32 v[20:21], v[20:21], v[22:23] neg_lo:[0,1] neg_hi:[0,1]
	ds_write_b64 v10, v[40:41]
	ds_write_b64 v13, v[24:25]
	ds_write_b64 v15, v[28:29]
	ds_write_b64 v52, v[18:19]
	ds_write_b64 v53, v[42:43]
	ds_write_b64 v54, v[46:47]
	ds_write_b64 v55, v[50:51]
	ds_write_b64 v56, v[44:45]
	ds_write_b64 v57, v[36:37]
	ds_write_b64 v58, v[26:27]
	ds_write_b64 v59, v[48:49]
	ds_write_b64 v60, v[32:33]
	ds_write_b64 v61, v[34:35]
	ds_write_b64 v62, v[30:31]
	ds_write_b64 v63, v[38:39]
	ds_write_b64 v64, v[20:21]
	v_mov_b32_e32 v10, v177
	v_mov_b32_e32 v64, v165
	v_lshlrev_b32_e32 v13, 3, v17
	v_lshlrev_b32_e32 v48, 3, v10
	v_add3_u32 v10, 0, v13, v48
	v_xor_b32_e32 v13, 1, v17
	v_xor_b32_e32 v34, 8, v17
	v_xor_b32_e32 v36, 9, v17
	v_lshlrev_b32_e32 v13, 3, v13
	v_xor_b32_e32 v15, 2, v17
	v_xor_b32_e32 v24, 3, v17
	v_xor_b32_e32 v26, 4, v17
	v_xor_b32_e32 v28, 5, v17
	v_xor_b32_e32 v30, 6, v17
	v_xor_b32_e32 v32, 7, v17
	v_lshlrev_b32_e32 v34, 3, v34
	v_lshlrev_b32_e32 v36, 3, v36
	v_xor_b32_e32 v38, 10, v17
	v_xor_b32_e32 v40, 11, v17
	v_xor_b32_e32 v42, 12, v17
	v_xor_b32_e32 v44, 13, v17
	v_xor_b32_e32 v46, 14, v17
	v_xor_b32_e32 v17, 15, v17
	v_add3_u32 v13, 0, v13, v48
	v_lshlrev_b32_e32 v15, 3, v15
	v_lshlrev_b32_e32 v24, 3, v24
	v_lshlrev_b32_e32 v26, 3, v26
	v_lshlrev_b32_e32 v28, 3, v28
	v_lshlrev_b32_e32 v30, 3, v30
	v_lshlrev_b32_e32 v32, 3, v32
	v_add3_u32 v55, 0, v34, v48
	v_add3_u32 v56, 0, v36, v48
	v_lshlrev_b32_e32 v38, 3, v38
	v_lshlrev_b32_e32 v40, 3, v40
	v_lshlrev_b32_e32 v42, 3, v42
	v_lshlrev_b32_e32 v44, 3, v44
	v_lshlrev_b32_e32 v46, 3, v46
	v_lshlrev_b32_e32 v17, 3, v17
	ds_read_b64 v[18:19], v10
	ds_read_b64 v[20:21], v13
	v_add3_u32 v15, 0, v15, v48
	v_add3_u32 v50, 0, v24, v48
	v_add3_u32 v51, 0, v26, v48
	v_add3_u32 v52, 0, v28, v48
	v_add3_u32 v53, 0, v30, v48
	v_add3_u32 v54, 0, v32, v48
	ds_read_b64 v[34:35], v55
	ds_read_b64 v[36:37], v56
	v_add3_u32 v57, 0, v38, v48
	v_add3_u32 v58, 0, v40, v48
	v_add3_u32 v59, 0, v42, v48
	v_add3_u32 v60, 0, v44, v48
	v_add3_u32 v61, 0, v46, v48
	v_add3_u32 v62, 0, v17, v48
	ds_read_b64 v[22:23], v15
	ds_read_b64 v[24:25], v50
	ds_read_b64 v[26:27], v51
	ds_read_b64 v[28:29], v52
	ds_read_b64 v[30:31], v53
	ds_read_b64 v[32:33], v54
	ds_read_b64 v[38:39], v57
	ds_read_b64 v[40:41], v58
	ds_read_b64 v[42:43], v59
	ds_read_b64 v[44:45], v60
	ds_read_b64 v[46:47], v61
	ds_read_b64 v[48:49], v62
	s_waitcnt lgkmcnt(13)
	v_pk_add_f32 v[70:71], v[18:19], v[34:35]
	v_pk_add_f32 v[18:19], v[18:19], v[34:35] neg_lo:[0,1] neg_hi:[0,1]
	s_waitcnt lgkmcnt(12)
	v_pk_add_f32 v[34:35], v[20:21], v[36:37]
	v_pk_add_f32 v[20:21], v[20:21], v[36:37] neg_lo:[0,1] neg_hi:[0,1]
	s_nop 0
	v_pk_mul_f32 v[36:37], v[20:21], v[68:69] op_sel:[1,0] op_sel_hi:[0,0] neg_lo:[1,1] neg_hi:[0,1]
	v_pk_fma_f32 v[20:21], v[20:21], v[64:65], v[36:37] op_sel_hi:[1,0,1]
	s_waitcnt lgkmcnt(5)
	v_pk_add_f32 v[36:37], v[22:23], v[38:39]
	v_pk_add_f32 v[22:23], v[22:23], v[38:39] neg_lo:[0,1] neg_hi:[0,1]
	s_nop 0
	v_pk_mul_f32 v[38:39], v[22:23], v[66:67] op_sel:[1,0] op_sel_hi:[0,0] neg_lo:[1,1] neg_hi:[0,1]
	v_pk_fma_f32 v[22:23], v[22:23], v[66:67], v[38:39] op_sel_hi:[1,0,1]
	s_waitcnt lgkmcnt(4)
	v_pk_add_f32 v[38:39], v[24:25], v[40:41]
	v_pk_add_f32 v[24:25], v[24:25], v[40:41] neg_lo:[0,1] neg_hi:[0,1]
	s_nop 0
	v_pk_mul_f32 v[40:41], v[24:25], v[68:69] op_sel_hi:[1,0]
	s_nop 0
	v_pk_fma_f32 v[24:25], v[24:25], v[64:65], v[40:41] op_sel:[1,0,0] op_sel_hi:[0,0,1] neg_lo:[1,1,0] neg_hi:[0,1,0]
	s_waitcnt lgkmcnt(3)
	v_pk_add_f32 v[40:41], v[26:27], v[42:43]
	v_pk_add_f32 v[26:27], v[26:27], v[42:43] neg_lo:[0,1] neg_hi:[0,1]
	s_nop 0
	v_xor_b32_e32 v73, 0x80000000, v26
	v_mov_b32_e32 v72, v27
	s_waitcnt lgkmcnt(2)
	v_pk_add_f32 v[26:27], v[28:29], v[44:45]
	v_pk_add_f32 v[28:29], v[28:29], v[44:45] neg_lo:[0,1] neg_hi:[0,1]
	s_nop 0
	v_pk_mul_f32 v[42:43], v[28:29], v[68:69] op_sel_hi:[1,0] neg_lo:[0,1] neg_hi:[0,1]
	s_nop 0
	v_pk_fma_f32 v[28:29], v[28:29], v[64:65], v[42:43] op_sel:[1,0,0] op_sel_hi:[0,0,1] neg_lo:[1,1,0] neg_hi:[0,1,0]
	s_waitcnt lgkmcnt(1)
	v_pk_add_f32 v[42:43], v[30:31], v[46:47]
	v_pk_add_f32 v[30:31], v[30:31], v[46:47] neg_lo:[0,1] neg_hi:[0,1]
	s_nop 0
	v_pk_mul_f32 v[44:45], v[30:31], v[66:67] op_sel:[1,0] op_sel_hi:[0,0] neg_lo:[1,1] neg_hi:[0,1]
	s_nop 0
	v_pk_fma_f32 v[30:31], v[30:31], v[66:67], v[44:45] op_sel_hi:[1,0,1] neg_lo:[0,1,0] neg_hi:[0,1,0]
	s_waitcnt lgkmcnt(0)
	v_pk_add_f32 v[44:45], v[32:33], v[48:49]
	v_pk_add_f32 v[32:33], v[32:33], v[48:49] neg_lo:[0,1] neg_hi:[0,1]
	v_pk_add_f32 v[48:49], v[34:35], v[26:27]
	v_pk_add_f32 v[26:27], v[34:35], v[26:27] neg_lo:[0,1] neg_hi:[0,1]
	s_nop 0
	v_pk_mul_f32 v[34:35], v[26:27], v[66:67] op_sel:[1,0] op_sel_hi:[0,0] neg_lo:[1,1] neg_hi:[0,1]
	v_pk_fma_f32 v[26:27], v[26:27], v[66:67], v[34:35] op_sel_hi:[1,0,1]
	v_pk_add_f32 v[34:35], v[36:37], v[42:43]
	v_pk_add_f32 v[36:37], v[36:37], v[42:43] neg_lo:[0,1] neg_hi:[0,1]
	v_pk_mul_f32 v[46:47], v[32:33], v[68:69] op_sel:[1,0] op_sel_hi:[0,0] neg_lo:[1,1] neg_hi:[0,1]
	v_xor_b32_e32 v43, 0x80000000, v36
	v_mov_b32_e32 v42, v37
	v_pk_add_f32 v[36:37], v[38:39], v[44:45]
	v_pk_add_f32 v[38:39], v[38:39], v[44:45] neg_lo:[0,1] neg_hi:[0,1]
	v_pk_fma_f32 v[46:47], v[32:33], v[64:65], v[46:47] op_sel_hi:[1,0,1] neg_lo:[0,1,0] neg_hi:[0,1,0]
	v_pk_add_f32 v[32:33], v[70:71], v[40:41]
	v_pk_mul_f32 v[44:45], v[38:39], v[66:67] op_sel:[1,0] op_sel_hi:[0,0] neg_lo:[1,1] neg_hi:[0,1]
	v_pk_add_f32 v[40:41], v[70:71], v[40:41] neg_lo:[0,1] neg_hi:[0,1]
	v_pk_fma_f32 v[38:39], v[38:39], v[66:67], v[44:45] op_sel_hi:[1,0,1] neg_lo:[0,1,0] neg_hi:[0,1,0]
	v_pk_add_f32 v[44:45], v[32:33], v[34:35]
	v_pk_add_f32 v[32:33], v[32:33], v[34:35] neg_lo:[0,1] neg_hi:[0,1]
	v_pk_add_f32 v[34:35], v[48:49], v[36:37]
	v_pk_add_f32 v[36:37], v[48:49], v[36:37] neg_lo:[0,1] neg_hi:[0,1]
	v_pk_add_f32 v[64:65], v[44:45], v[34:35]
	v_xor_b32_e32 v49, 0x80000000, v36
	v_mov_b32_e32 v48, v37
	v_pk_add_f32 v[36:37], v[44:45], v[34:35] neg_lo:[0,1] neg_hi:[0,1]
	v_pk_add_f32 v[68:69], v[32:33], v[48:49]
	v_pk_add_f32 v[44:45], v[32:33], v[48:49] neg_lo:[0,1] neg_hi:[0,1]
	v_pk_add_f32 v[32:33], v[40:41], v[42:43]
	v_pk_add_f32 v[34:35], v[40:41], v[42:43] neg_lo:[0,1] neg_hi:[0,1]
	v_pk_add_f32 v[40:41], v[26:27], v[38:39]
	v_pk_add_f32 v[26:27], v[26:27], v[38:39] neg_lo:[0,1] neg_hi:[0,1]
	v_pk_add_f32 v[42:43], v[32:33], v[40:41] neg_lo:[0,1] neg_hi:[0,1]
	v_xor_b32_e32 v39, 0x80000000, v26
	v_mov_b32_e32 v38, v27
	v_pk_add_f32 v[26:27], v[32:33], v[40:41]
	v_pk_add_f32 v[40:41], v[20:21], v[28:29]
	v_pk_add_f32 v[20:21], v[20:21], v[28:29] neg_lo:[0,1] neg_hi:[0,1]
	v_pk_add_f32 v[32:33], v[34:35], v[38:39]
	v_pk_mul_f32 v[28:29], v[66:67], v[20:21] op_sel:[0,1] op_sel_hi:[0,0] neg_lo:[1,1] neg_hi:[1,0]
	v_pk_fma_f32 v[20:21], v[66:67], v[20:21], v[28:29] op_sel_hi:[0,1,1]
	v_pk_add_f32 v[28:29], v[22:23], v[30:31]
	v_pk_add_f32 v[22:23], v[22:23], v[30:31] neg_lo:[0,1] neg_hi:[0,1]
	v_pk_add_f32 v[38:39], v[34:35], v[38:39] neg_lo:[0,1] neg_hi:[0,1]
	v_xor_b32_e32 v31, 0x80000000, v22
	v_mov_b32_e32 v30, v23
	v_pk_add_f32 v[22:23], v[24:25], v[46:47]
	v_pk_add_f32 v[24:25], v[24:25], v[46:47] neg_lo:[0,1] neg_hi:[0,1]
	v_pk_add_f32 v[34:35], v[18:19], v[72:73]
	v_pk_mul_f32 v[46:47], v[66:67], v[24:25] op_sel:[0,1] op_sel_hi:[0,0] neg_lo:[1,1] neg_hi:[1,0]
	v_pk_fma_f32 v[24:25], v[66:67], v[24:25], v[46:47] op_sel_hi:[0,1,1] neg_lo:[1,0,0] neg_hi:[1,0,0]
	v_pk_add_f32 v[46:47], v[34:35], v[28:29]
	v_pk_add_f32 v[28:29], v[34:35], v[28:29] neg_lo:[0,1] neg_hi:[0,1]
	v_pk_add_f32 v[34:35], v[40:41], v[22:23]
	v_pk_add_f32 v[22:23], v[40:41], v[22:23] neg_lo:[0,1] neg_hi:[0,1]
	v_pk_add_f32 v[18:19], v[18:19], v[72:73] neg_lo:[0,1] neg_hi:[0,1]
	v_pk_add_f32 v[66:67], v[28:29], v[22:23] op_sel:[0,1] op_sel_hi:[1,0] neg_hi:[0,1]
	v_pk_add_f32 v[48:49], v[28:29], v[22:23] op_sel:[0,1] op_sel_hi:[1,0] neg_lo:[0,1]
	v_pk_add_f32 v[28:29], v[18:19], v[30:31]
	v_pk_add_f32 v[18:19], v[18:19], v[30:31] neg_lo:[0,1] neg_hi:[0,1]
	v_pk_add_f32 v[30:31], v[20:21], v[24:25]
	v_pk_add_f32 v[20:21], v[20:21], v[24:25] neg_lo:[0,1] neg_hi:[0,1]
	v_pk_add_f32 v[22:23], v[46:47], v[34:35]
	v_xor_b32_e32 v25, 0x80000000, v20
	v_mov_b32_e32 v24, v21
	s_waitcnt vmcnt(0)
	v_pk_add_f32 v[40:41], v[46:47], v[34:35] neg_lo:[0,1] neg_hi:[0,1]
	v_pk_add_f32 v[34:35], v[18:19], v[24:25]
	v_pk_add_f32 v[18:19], v[18:19], v[24:25] neg_lo:[0,1] neg_hi:[0,1]
	v_pk_add_f32 v[70:71], v[28:29], v[30:31]
	v_pk_add_f32 v[46:47], v[28:29], v[30:31] neg_lo:[0,1] neg_hi:[0,1]
	s_nop 0
	v_pk_mul_f32 v[24:25], v[64:65], v[202:203] op_sel:[1,1] op_sel_hi:[1,0] neg_lo:[1,0]
	s_nop 0
	v_pk_fma_f32 v[20:21], v[64:65], v[202:203], v[24:25] op_sel_hi:[0,1,1]
	s_nop 0
	v_pk_mul_f32 v[28:29], v[204:205], v[22:23] op_sel:[1,1] op_sel_hi:[0,1] neg_lo:[0,1]
	v_pk_fma_f32 v[22:23], v[204:205], v[22:23], v[28:29] op_sel_hi:[1,0,1]
	s_nop 0
	v_pk_mul_f32 v[28:29], v[26:27], v[206:207] op_sel:[1,1] op_sel_hi:[1,0] neg_lo:[1,0]
	s_nop 0
	v_pk_fma_f32 v[24:25], v[26:27], v[206:207], v[28:29] op_sel_hi:[0,1,1]
	s_nop 0
	v_pk_mul_f32 v[28:29], v[208:209], v[70:71] op_sel:[1,1] op_sel_hi:[0,1] neg_lo:[0,1]
	v_pk_fma_f32 v[26:27], v[208:209], v[70:71], v[28:29] op_sel_hi:[1,0,1]
	s_nop 0
	v_pk_mul_f32 v[30:31], v[68:69], v[210:211] op_sel:[1,1] op_sel_hi:[1,0] neg_lo:[1,0]
	s_nop 0
	v_pk_fma_f32 v[28:29], v[68:69], v[210:211], v[30:31] op_sel_hi:[0,1,1]
	s_nop 0
	v_pk_mul_f32 v[64:65], v[212:213], v[66:67] op_sel:[1,1] op_sel_hi:[0,1] neg_lo:[0,1]
	v_pk_fma_f32 v[30:31], v[212:213], v[66:67], v[64:65] op_sel_hi:[1,0,1]
	s_nop 0
	v_pk_mul_f32 v[66:67], v[32:33], v[214:215] op_sel:[1,1] op_sel_hi:[1,0] neg_lo:[1,0]
	s_nop 0
	v_pk_fma_f32 v[32:33], v[32:33], v[214:215], v[66:67] op_sel_hi:[0,1,1]
	s_nop 0
	v_pk_mul_f32 v[66:67], v[216:217], v[34:35] op_sel:[1,1] op_sel_hi:[0,1] neg_lo:[0,1]
	v_pk_fma_f32 v[34:35], v[216:217], v[34:35], v[66:67] op_sel_hi:[1,0,1]
	s_nop 0
	v_pk_mul_f32 v[66:67], v[36:37], v[218:219] op_sel:[1,1] op_sel_hi:[1,0] neg_lo:[1,0]
	s_nop 0
	v_pk_fma_f32 v[36:37], v[36:37], v[218:219], v[66:67] op_sel_hi:[0,1,1]
	v_pk_add_f32 v[68:69], v[20:21], v[36:37]
	v_pk_add_f32 v[20:21], v[20:21], v[36:37] neg_lo:[0,1] neg_hi:[0,1]
	s_nop 0
	v_pk_mul_f32 v[66:67], v[40:41], v[220:221] op_sel:[1,1] op_sel_hi:[1,0] neg_lo:[1,0]
	s_nop 0
	v_pk_fma_f32 v[40:41], v[40:41], v[220:221], v[66:67] op_sel_hi:[0,1,1]
	v_pk_add_f32 v[36:37], v[22:23], v[40:41]
	v_pk_add_f32 v[22:23], v[22:23], v[40:41] neg_lo:[0,1] neg_hi:[0,1]
	s_nop 0
	v_pk_mul_f32 v[66:67], v[42:43], v[222:223] op_sel:[1,1] op_sel_hi:[1,0] neg_lo:[1,0]
	s_nop 0
	v_pk_fma_f32 v[42:43], v[42:43], v[222:223], v[66:67] op_sel_hi:[0,1,1]
	s_nop 0
	v_pk_mul_f32 v[66:67], v[46:47], v[224:225] op_sel:[1,1] op_sel_hi:[1,0] neg_lo:[1,0]
	s_nop 0
	v_pk_fma_f32 v[46:47], v[46:47], v[224:225], v[66:67] op_sel_hi:[0,1,1]
	s_nop 0
	v_pk_mul_f32 v[66:67], v[44:45], v[226:227] op_sel:[1,1] op_sel_hi:[1,0] neg_lo:[1,0]
	s_nop 0
	v_pk_fma_f32 v[44:45], v[44:45], v[226:227], v[66:67] op_sel_hi:[0,1,1]
	s_nop 0
	v_pk_mul_f32 v[66:67], v[48:49], v[228:229] op_sel:[1,1] op_sel_hi:[1,0] neg_lo:[1,0]
	s_nop 0
	v_pk_fma_f32 v[48:49], v[48:49], v[228:229], v[66:67] op_sel_hi:[0,1,1]
	s_nop 0
	v_pk_mul_f32 v[66:67], v[38:39], v[230:231] op_sel:[1,1] op_sel_hi:[1,0] neg_lo:[1,0]
	s_nop 0
	v_pk_fma_f32 v[38:39], v[38:39], v[230:231], v[66:67] op_sel_hi:[0,1,1]
	s_nop 0
	v_pk_mul_f32 v[64:65], v[18:19], v[232:233] op_sel:[1,1] op_sel_hi:[1,0] neg_lo:[1,0]
	v_mov_b32_e32 v66, v169
	v_pk_fma_f32 v[16:17], v[18:19], v[232:233], v[64:65] op_sel_hi:[0,1,1]
	v_mov_b32_e32 v64, v167
	v_mov_b32_e32 v18, v165
	s_nop 0
	s_nop 0
	v_pk_mul_f32 v[40:41], v[22:23], v[66:67] op_sel:[1,0] op_sel_hi:[0,0] neg_lo:[1,0]
	v_mov_b32_e32 v19, v171
	s_nop 0
	v_pk_fma_f32 v[22:23], v[22:23], v[18:19], v[40:41] op_sel_hi:[1,0,1]
	v_pk_add_f32 v[40:41], v[24:25], v[42:43]
	v_pk_add_f32 v[24:25], v[24:25], v[42:43] neg_lo:[0,1] neg_hi:[0,1]
	s_nop 0
	v_pk_mul_f32 v[42:43], v[24:25], v[64:65] op_sel:[1,0] op_sel_hi:[0,0] neg_lo:[1,0]
	s_nop 0
	v_pk_fma_f32 v[24:25], v[24:25], v[64:65], v[42:43] op_sel_hi:[1,0,1]
	v_pk_add_f32 v[42:43], v[26:27], v[46:47]
	v_pk_add_f32 v[26:27], v[26:27], v[46:47] neg_lo:[0,1] neg_hi:[0,1]
	s_nop 0
	v_pk_mul_f32 v[46:47], v[26:27], v[66:67] op_sel_hi:[1,0]
	s_nop 0
	v_pk_fma_f32 v[26:27], v[26:27], v[18:19], v[46:47] op_sel:[1,0,0] op_sel_hi:[0,0,1] neg_lo:[1,0,0]
	v_pk_add_f32 v[46:47], v[28:29], v[44:45]
	v_pk_add_f32 v[28:29], v[28:29], v[44:45] neg_lo:[0,1] neg_hi:[0,1]
	s_nop 0
	v_xor_b32_e32 v44, 0x80000000, v29
	v_mov_b32_e32 v45, v28
	v_pk_add_f32 v[28:29], v[30:31], v[48:49]
	v_pk_add_f32 v[30:31], v[30:31], v[48:49] neg_lo:[0,1] neg_hi:[0,1]
	s_nop 0
	v_pk_mul_f32 v[48:49], v[30:31], v[66:67] op_sel_hi:[1,0] neg_lo:[0,1] neg_hi:[0,1]
	s_nop 0
	v_pk_fma_f32 v[30:31], v[30:31], v[18:19], v[48:49] op_sel:[1,0,0] op_sel_hi:[0,0,1] neg_lo:[1,0,0]
	v_pk_add_f32 v[48:49], v[32:33], v[38:39]
	v_pk_add_f32 v[32:33], v[32:33], v[38:39] neg_lo:[0,1] neg_hi:[0,1]
	s_nop 0
	v_pk_mul_f32 v[38:39], v[32:33], v[64:65] op_sel:[1,0] op_sel_hi:[0,0] neg_lo:[1,0]
	s_nop 0
	v_pk_fma_f32 v[32:33], v[32:33], v[64:65], v[38:39] op_sel_hi:[1,0,1] neg_lo:[0,1,0] neg_hi:[0,1,0]
	v_pk_add_f32 v[38:39], v[34:35], v[16:17]
	v_pk_add_f32 v[16:17], v[34:35], v[16:17] neg_lo:[0,1] neg_hi:[0,1]
	s_nop 0
	v_pk_mul_f32 v[34:35], v[16:17], v[66:67] op_sel:[1,0] op_sel_hi:[0,0] neg_lo:[1,0]
	s_nop 0
	v_pk_fma_f32 v[16:17], v[16:17], v[18:19], v[34:35] op_sel_hi:[1,0,1] neg_lo:[0,1,0] neg_hi:[0,1,0]
	v_pk_add_f32 v[18:19], v[68:69], v[46:47]
	v_pk_add_f32 v[34:35], v[68:69], v[46:47] neg_lo:[0,1] neg_hi:[0,1]
	v_pk_add_f32 v[46:47], v[36:37], v[28:29]
	v_pk_add_f32 v[28:29], v[36:37], v[28:29] neg_lo:[0,1] neg_hi:[0,1]
	s_nop 0
	v_pk_mul_f32 v[36:37], v[28:29], v[64:65] op_sel:[1,0] op_sel_hi:[0,0] neg_lo:[1,0]
	s_nop 0
	v_pk_fma_f32 v[28:29], v[28:29], v[64:65], v[36:37] op_sel_hi:[1,0,1]
	v_pk_add_f32 v[36:37], v[40:41], v[48:49]
	v_pk_add_f32 v[40:41], v[40:41], v[48:49] neg_lo:[0,1] neg_hi:[0,1]
	s_nop 0
	v_xor_b32_e32 v48, 0x80000000, v41
	v_mov_b32_e32 v49, v40
	v_pk_add_f32 v[40:41], v[42:43], v[38:39]
	v_pk_add_f32 v[38:39], v[42:43], v[38:39] neg_lo:[0,1] neg_hi:[0,1]
	s_nop 0
	v_pk_mul_f32 v[42:43], v[64:65], v[38:39] op_sel:[0,1] op_sel_hi:[0,0] neg_lo:[0,1]
	v_pk_fma_f32 v[38:39], v[38:39], v[64:65], v[42:43] op_sel_hi:[1,0,1] neg_lo:[0,1,0] neg_hi:[0,1,0]
	v_pk_add_f32 v[42:43], v[18:19], v[36:37]
	v_pk_add_f32 v[18:19], v[18:19], v[36:37] neg_lo:[0,1] neg_hi:[0,1]
	v_pk_add_f32 v[36:37], v[46:47], v[40:41]
	v_pk_add_f32 v[40:41], v[46:47], v[40:41] neg_lo:[0,1] neg_hi:[0,1]
	s_nop 0
	v_xor_b32_e32 v46, 0x80000000, v41
	v_mov_b32_e32 v47, v40
	v_pk_add_f32 v[40:41], v[42:43], v[36:37]
	v_pk_add_f32 v[36:37], v[42:43], v[36:37] neg_lo:[0,1] neg_hi:[0,1]
	v_pk_add_f32 v[42:43], v[18:19], v[46:47]
	v_pk_add_f32 v[18:19], v[18:19], v[46:47] neg_lo:[0,1] neg_hi:[0,1]
	v_pk_add_f32 v[46:47], v[34:35], v[48:49]
	v_pk_add_f32 v[34:35], v[34:35], v[48:49] neg_lo:[0,1] neg_hi:[0,1]
	v_pk_add_f32 v[48:49], v[28:29], v[38:39]
	v_pk_add_f32 v[28:29], v[28:29], v[38:39] neg_lo:[0,1] neg_hi:[0,1]
	s_nop 0
	v_xor_b32_e32 v38, 0x80000000, v29
	v_mov_b32_e32 v39, v28
	v_pk_add_f32 v[28:29], v[46:47], v[48:49]
	v_pk_add_f32 v[46:47], v[46:47], v[48:49] neg_lo:[0,1] neg_hi:[0,1]
	v_pk_add_f32 v[48:49], v[34:35], v[38:39]
	v_pk_add_f32 v[34:35], v[34:35], v[38:39] neg_lo:[0,1] neg_hi:[0,1]
	v_pk_add_f32 v[38:39], v[20:21], v[44:45]
	v_pk_add_f32 v[20:21], v[20:21], v[44:45] neg_lo:[0,1] neg_hi:[0,1]
	v_pk_add_f32 v[44:45], v[22:23], v[30:31]
	v_pk_add_f32 v[22:23], v[22:23], v[30:31] neg_lo:[0,1] neg_hi:[0,1]
	s_nop 0
	v_pk_mul_f32 v[30:31], v[64:65], v[22:23] op_sel:[0,1] op_sel_hi:[0,0] neg_lo:[0,1]
	v_pk_fma_f32 v[22:23], v[64:65], v[22:23], v[30:31] op_sel_hi:[0,1,1]
	v_pk_add_f32 v[30:31], v[24:25], v[32:33]
	v_pk_add_f32 v[24:25], v[24:25], v[32:33] neg_lo:[0,1] neg_hi:[0,1]
	s_nop 0
	v_xor_b32_e32 v32, 0x80000000, v25
	v_mov_b32_e32 v33, v24
	v_pk_add_f32 v[24:25], v[26:27], v[16:17]
	v_pk_add_f32 v[16:17], v[26:27], v[16:17] neg_lo:[0,1] neg_hi:[0,1]
	s_nop 0
	v_pk_mul_f32 v[26:27], v[64:65], v[16:17] op_sel:[0,1] op_sel_hi:[0,0] neg_lo:[0,1]
	v_pk_fma_f32 v[16:17], v[64:65], v[16:17], v[26:27] op_sel_hi:[0,1,1] neg_lo:[1,0,0] neg_hi:[1,0,0]
	v_pk_add_f32 v[26:27], v[38:39], v[30:31]
	v_pk_add_f32 v[30:31], v[38:39], v[30:31] neg_lo:[0,1] neg_hi:[0,1]
	v_pk_add_f32 v[38:39], v[44:45], v[24:25]
	v_pk_add_f32 v[24:25], v[44:45], v[24:25] neg_lo:[0,1] neg_hi:[0,1]
	s_nop 0
	v_xor_b32_e32 v44, 0x80000000, v25
	v_mov_b32_e32 v45, v24
	v_pk_add_f32 v[24:25], v[26:27], v[38:39]
	v_pk_add_f32 v[26:27], v[26:27], v[38:39] neg_lo:[0,1] neg_hi:[0,1]
	v_pk_add_f32 v[38:39], v[30:31], v[44:45]
	v_pk_add_f32 v[30:31], v[30:31], v[44:45] neg_lo:[0,1] neg_hi:[0,1]
	v_pk_add_f32 v[44:45], v[20:21], v[32:33]
	v_pk_add_f32 v[20:21], v[20:21], v[32:33] neg_lo:[0,1] neg_hi:[0,1]
	v_pk_add_f32 v[32:33], v[22:23], v[16:17]
	v_pk_add_f32 v[16:17], v[22:23], v[16:17] neg_lo:[0,1] neg_hi:[0,1]
	s_nop 0
	v_xor_b32_e32 v22, 0x80000000, v17
	v_mov_b32_e32 v23, v16
	v_pk_add_f32 v[16:17], v[44:45], v[32:33]
	v_pk_add_f32 v[32:33], v[44:45], v[32:33] neg_lo:[0,1] neg_hi:[0,1]
	v_pk_add_f32 v[44:45], v[20:21], v[22:23]
	v_pk_add_f32 v[20:21], v[20:21], v[22:23] neg_lo:[0,1] neg_hi:[0,1]
	ds_write_b64 v10, v[40:41]
	ds_write_b64 v13, v[24:25]
	ds_write_b64 v15, v[28:29]
	ds_write_b64 v50, v[16:17]
	ds_write_b64 v51, v[42:43]
	ds_write_b64 v52, v[38:39]
	ds_write_b64 v53, v[48:49]
	ds_write_b64 v54, v[44:45]
	ds_write_b64 v55, v[36:37]
	ds_write_b64 v56, v[26:27]
	ds_write_b64 v57, v[46:47]
	ds_write_b64 v58, v[32:33]
	ds_write_b64 v59, v[18:19]
	ds_write_b64 v60, v[30:31]
	ds_write_b64 v61, v[34:35]
	ds_write_b64 v62, v[20:21]
	v_mov_b32_e32 v10, v174
	v_mov_b32_e32 v50, v172
	s_waitcnt lgkmcnt(0)
	s_barrier
	v_add_u32_e32 v13, v50, v10
	v_lshl_add_u32 v13, v13, 3, 0
	ds_read2_b64 v[16:19], v13 offset1:16
	v_xad_u32 v15, v50, 1, v10
	v_lshl_add_u32 v15, v15, 3, 0
	s_waitcnt lgkmcnt(0)
	v_pk_fma_f32 v[16:17], v[16:17], 0, v[16:17] op_sel:[1,0,0] op_sel_hi:[0,0,1] neg_hi:[1,0,0]
	v_pk_fma_f32 v[22:23], v[180:181], s[90:91], v[180:181] op_sel:[1,0,0] op_sel_hi:[0,1,1]
	v_pk_mul_f32 v[24:25], v[22:23], v[18:19] op_sel:[1,1] op_sel_hi:[1,0] neg_hi:[0,1]
	s_nop 0
	v_pk_fma_f32 v[18:19], v[18:19], v[22:23], v[24:25] op_sel_hi:[1,0,1]
	v_pk_mul_f32 v[24:25], v[180:181], v[22:23] op_sel:[1,1] op_sel_hi:[0,1] neg_lo:[0,1]
	v_pk_fma_f32 v[26:27], v[180:181], v[22:23], v[24:25] op_sel_hi:[1,0,1]
	ds_read2_b64 v[22:25], v15 offset0:32 offset1:48
	s_waitcnt lgkmcnt(0)
	v_pk_mul_f32 v[28:29], v[22:23], v[26:27] op_sel:[1,1] op_sel_hi:[0,1] neg_hi:[1,0]
	s_nop 0
	v_pk_fma_f32 v[22:23], v[22:23], v[26:27], v[28:29] op_sel_hi:[1,0,1]
	v_pk_mul_f32 v[28:29], v[180:181], v[26:27] op_sel:[1,1] op_sel_hi:[0,1] neg_lo:[0,1]
	v_pk_fma_f32 v[26:27], v[180:181], v[26:27], v[28:29] op_sel_hi:[1,0,1]
	s_nop 0
	v_pk_mul_f32 v[28:29], v[24:25], v[26:27] op_sel:[1,1] op_sel_hi:[0,1] neg_hi:[1,0]
	s_nop 0
	v_pk_fma_f32 v[24:25], v[24:25], v[26:27], v[28:29] op_sel_hi:[1,0,1]
	v_pk_mul_f32 v[28:29], v[180:181], v[26:27] op_sel:[1,1] op_sel_hi:[0,1] neg_lo:[0,1]
	v_pk_fma_f32 v[26:27], v[180:181], v[26:27], v[28:29] op_sel_hi:[1,0,1]
	v_xad_u32 v28, v50, 2, v10
	v_lshl_add_u32 v51, v28, 3, 0
	ds_read2_b64 v[28:31], v51 offset0:64 offset1:80
	v_pk_mul_f32 v[32:33], v[180:181], v[26:27] op_sel:[1,1] op_sel_hi:[0,1] neg_lo:[0,1]
	s_waitcnt lgkmcnt(0)
	v_pk_mul_f32 v[34:35], v[28:29], v[26:27] op_sel:[1,1] op_sel_hi:[0,1] neg_hi:[1,0]
	s_nop 0
	v_pk_fma_f32 v[28:29], v[28:29], v[26:27], v[34:35] op_sel_hi:[1,0,1]
	v_pk_fma_f32 v[34:35], v[180:181], v[26:27], v[32:33] op_sel_hi:[1,0,1]
	s_nop 0
	v_pk_mul_f32 v[26:27], v[30:31], v[34:35] op_sel:[1,1] op_sel_hi:[0,1] neg_hi:[1,0]
	v_pk_fma_f32 v[26:27], v[30:31], v[34:35], v[26:27] op_sel_hi:[1,0,1]
	v_xad_u32 v30, v50, 3, v10
	v_lshl_add_u32 v54, v30, 3, 0
	ds_read2_b64 v[30:33], v54 offset0:96 offset1:112
	v_pk_mul_f32 v[36:37], v[180:181], v[34:35] op_sel:[1,1] op_sel_hi:[0,1] neg_lo:[0,1]
	v_pk_fma_f32 v[34:35], v[180:181], v[34:35], v[36:37] op_sel_hi:[1,0,1]
	s_waitcnt lgkmcnt(0)
	v_pk_mul_f32 v[36:37], v[30:31], v[34:35] op_sel:[1,1] op_sel_hi:[0,1] neg_hi:[1,0]
	s_nop 0
	v_pk_fma_f32 v[30:31], v[30:31], v[34:35], v[36:37] op_sel_hi:[1,0,1]
	v_pk_mul_f32 v[36:37], v[180:181], v[34:35] op_sel:[1,1] op_sel_hi:[0,1] neg_lo:[0,1]
	v_pk_fma_f32 v[34:35], v[180:181], v[34:35], v[36:37] op_sel_hi:[1,0,1]
	s_nop 0
	v_pk_mul_f32 v[36:37], v[32:33], v[34:35] op_sel:[1,1] op_sel_hi:[0,1] neg_hi:[1,0]
	s_nop 0
	v_pk_fma_f32 v[32:33], v[32:33], v[34:35], v[36:37] op_sel_hi:[1,0,1]
	v_pk_mul_f32 v[36:37], v[180:181], v[34:35] op_sel:[1,1] op_sel_hi:[0,1] neg_lo:[0,1]
	v_pk_fma_f32 v[38:39], v[180:181], v[34:35], v[36:37] op_sel_hi:[1,0,1]
	v_xad_u32 v34, v50, 4, v10
	v_lshl_add_u32 v55, v34, 3, 0
	ds_read2_b64 v[34:37], v55 offset0:128 offset1:144
	v_pk_mul_f32 v[40:41], v[180:181], v[38:39] op_sel:[1,1] op_sel_hi:[0,1] neg_lo:[0,1]
	s_waitcnt lgkmcnt(0)
	v_pk_mul_f32 v[42:43], v[34:35], v[38:39] op_sel:[1,1] op_sel_hi:[0,1] neg_hi:[1,0]
	s_nop 0
	v_pk_fma_f32 v[34:35], v[34:35], v[38:39], v[42:43] op_sel_hi:[1,0,1]
	v_pk_fma_f32 v[42:43], v[180:181], v[38:39], v[40:41] op_sel_hi:[1,0,1]
	s_nop 0
	v_pk_mul_f32 v[38:39], v[36:37], v[42:43] op_sel:[1,1] op_sel_hi:[0,1] neg_hi:[1,0]
	v_pk_fma_f32 v[36:37], v[36:37], v[42:43], v[38:39] op_sel_hi:[1,0,1]
	v_xad_u32 v38, v50, 5, v10
	v_lshl_add_u32 v56, v38, 3, 0
	ds_read2_b64 v[38:41], v56 offset0:160 offset1:176
	v_pk_mul_f32 v[44:45], v[180:181], v[42:43] op_sel:[1,1] op_sel_hi:[0,1] neg_lo:[0,1]
	v_pk_fma_f32 v[42:43], v[180:181], v[42:43], v[44:45] op_sel_hi:[1,0,1]
	s_waitcnt lgkmcnt(0)
	v_pk_mul_f32 v[44:45], v[38:39], v[42:43] op_sel:[1,1] op_sel_hi:[0,1] neg_hi:[1,0]
	s_nop 0
	v_pk_fma_f32 v[38:39], v[38:39], v[42:43], v[44:45] op_sel_hi:[1,0,1]
	v_pk_mul_f32 v[44:45], v[180:181], v[42:43] op_sel:[1,1] op_sel_hi:[0,1] neg_lo:[0,1]
	v_pk_fma_f32 v[42:43], v[180:181], v[42:43], v[44:45] op_sel_hi:[1,0,1]
	s_nop 0
	v_pk_mul_f32 v[44:45], v[40:41], v[42:43] op_sel:[1,1] op_sel_hi:[0,1] neg_hi:[1,0]
	s_nop 0
	v_pk_fma_f32 v[40:41], v[40:41], v[42:43], v[44:45] op_sel_hi:[1,0,1]
	v_pk_mul_f32 v[44:45], v[180:181], v[42:43] op_sel:[1,1] op_sel_hi:[0,1] neg_lo:[0,1]
	v_pk_fma_f32 v[42:43], v[180:181], v[42:43], v[44:45] op_sel_hi:[1,0,1]
	v_xad_u32 v44, v50, 6, v10
	v_lshl_add_u32 v57, v44, 3, 0
	ds_read2_b64 v[44:47], v57 offset0:192 offset1:208
	v_pk_mul_f32 v[48:49], v[180:181], v[42:43] op_sel:[1,1] op_sel_hi:[0,1] neg_lo:[0,1]
	s_waitcnt lgkmcnt(0)
	v_pk_mul_f32 v[52:53], v[44:45], v[42:43] op_sel:[1,1] op_sel_hi:[0,1] neg_hi:[1,0]
	s_nop 0
	v_pk_fma_f32 v[44:45], v[44:45], v[42:43], v[52:53] op_sel_hi:[1,0,1]
	v_pk_fma_f32 v[52:53], v[180:181], v[42:43], v[48:49] op_sel_hi:[1,0,1]
	s_nop 0
	v_pk_mul_f32 v[42:43], v[46:47], v[52:53] op_sel:[1,1] op_sel_hi:[0,1] neg_hi:[1,0]
	v_pk_fma_f32 v[42:43], v[46:47], v[52:53], v[42:43] op_sel_hi:[1,0,1]
	v_xad_u32 v46, v50, 7, v10
	v_lshl_add_u32 v58, v46, 3, 0
	ds_read2_b64 v[46:49], v58 offset0:224 offset1:240
	v_pk_mul_f32 v[60:61], v[180:181], v[52:53] op_sel:[1,1] op_sel_hi:[0,1] neg_lo:[0,1]
	v_pk_fma_f32 v[52:53], v[180:181], v[52:53], v[60:61] op_sel_hi:[1,0,1]
	s_waitcnt lgkmcnt(0)
	v_pk_mul_f32 v[60:61], v[46:47], v[52:53] op_sel:[1,1] op_sel_hi:[0,1] neg_hi:[1,0]
	s_nop 0
	v_pk_fma_f32 v[46:47], v[46:47], v[52:53], v[60:61] op_sel_hi:[1,0,1]
	v_pk_mul_f32 v[60:61], v[180:181], v[52:53] op_sel:[1,1] op_sel_hi:[0,1] neg_lo:[0,1]
	v_pk_fma_f32 v[52:53], v[180:181], v[52:53], v[60:61] op_sel_hi:[1,0,1]
	s_nop 0
	v_pk_mul_f32 v[60:61], v[48:49], v[52:53] op_sel:[1,1] op_sel_hi:[0,1] neg_hi:[1,0]
	s_nop 0
	v_pk_fma_f32 v[48:49], v[48:49], v[52:53], v[60:61] op_sel_hi:[1,0,1]
	v_pk_mul_f32 v[60:61], v[180:181], v[52:53] op_sel:[1,1] op_sel_hi:[0,1] neg_lo:[0,1]
	v_pk_fma_f32 v[64:65], v[180:181], v[52:53], v[60:61] op_sel_hi:[1,0,1]
	v_xad_u32 v52, v50, 8, v10
	v_lshl_add_u32 v52, v52, 3, 0
	v_add_u32_e32 v59, 0x800, v52
	ds_read2_b64 v[60:63], v59 offset1:16
	v_pk_mul_f32 v[66:67], v[180:181], v[64:65] op_sel:[1,1] op_sel_hi:[0,1] neg_lo:[0,1]
	v_pk_fma_f32 v[66:67], v[180:181], v[64:65], v[66:67] op_sel_hi:[1,0,1]
	s_waitcnt lgkmcnt(0)
	v_pk_mul_f32 v[52:53], v[60:61], v[64:65] op_sel:[1,1] op_sel_hi:[0,1] neg_hi:[1,0]
	v_pk_fma_f32 v[52:53], v[60:61], v[64:65], v[52:53] op_sel_hi:[1,0,1]
	v_pk_mul_f32 v[60:61], v[62:63], v[66:67] op_sel:[1,1] op_sel_hi:[0,1] neg_hi:[1,0]
	v_pk_fma_f32 v[70:71], v[62:63], v[66:67], v[60:61] op_sel_hi:[1,0,1]
	v_xad_u32 v60, v50, 9, v10
	v_lshl_add_u32 v60, v60, 3, 0
	v_add_u32_e32 v60, 0x800, v60
	ds_read2_b64 v[62:65], v60 offset0:32 offset1:48
	v_pk_mul_f32 v[68:69], v[180:181], v[66:67] op_sel:[1,1] op_sel_hi:[0,1] neg_lo:[0,1]
	v_pk_fma_f32 v[66:67], v[180:181], v[66:67], v[68:69] op_sel_hi:[1,0,1]
	s_waitcnt lgkmcnt(0)
	v_pk_mul_f32 v[68:69], v[62:63], v[66:67] op_sel:[1,1] op_sel_hi:[0,1] neg_hi:[1,0]
	s_nop 0
	v_pk_fma_f32 v[72:73], v[62:63], v[66:67], v[68:69] op_sel_hi:[1,0,1]
	v_pk_mul_f32 v[62:63], v[180:181], v[66:67] op_sel:[1,1] op_sel_hi:[0,1] neg_lo:[0,1]
	v_pk_fma_f32 v[62:63], v[180:181], v[66:67], v[62:63] op_sel_hi:[1,0,1]
	s_nop 0
	v_pk_mul_f32 v[66:67], v[64:65], v[62:63] op_sel:[1,1] op_sel_hi:[0,1] neg_hi:[1,0]
	s_nop 0
	v_pk_fma_f32 v[74:75], v[64:65], v[62:63], v[66:67] op_sel_hi:[1,0,1]
	v_pk_mul_f32 v[64:65], v[180:181], v[62:63] op_sel:[1,1] op_sel_hi:[0,1] neg_lo:[0,1]
	v_pk_fma_f32 v[66:67], v[180:181], v[62:63], v[64:65] op_sel_hi:[1,0,1]
	v_xad_u32 v61, v50, 10, v10
	v_lshl_add_u32 v61, v61, 3, 0
	v_add_u32_e32 v61, 0x800, v61
	ds_read2_b64 v[62:65], v61 offset0:64 offset1:80
	v_pk_mul_f32 v[68:69], v[180:181], v[66:67] op_sel:[1,1] op_sel_hi:[0,1] neg_lo:[0,1]
	v_pk_fma_f32 v[68:69], v[180:181], v[66:67], v[68:69] op_sel_hi:[1,0,1]
	s_waitcnt lgkmcnt(0)
	v_pk_mul_f32 v[76:77], v[62:63], v[66:67] op_sel:[1,1] op_sel_hi:[0,1] neg_hi:[1,0]
	v_pk_fma_f32 v[76:77], v[62:63], v[66:67], v[76:77] op_sel_hi:[1,0,1]
	v_pk_mul_f32 v[62:63], v[64:65], v[68:69] op_sel:[1,1] op_sel_hi:[0,1] neg_hi:[1,0]
	v_pk_fma_f32 v[78:79], v[64:65], v[68:69], v[62:63] op_sel_hi:[1,0,1]
	v_xad_u32 v62, v50, 11, v10
	v_lshl_add_u32 v62, v62, 3, 0
	v_add_u32_e32 v62, 0x800, v62
	ds_read2_b64 v[64:67], v62 offset0:96 offset1:112
	v_pk_mul_f32 v[80:81], v[180:181], v[68:69] op_sel:[1,1] op_sel_hi:[0,1] neg_lo:[0,1]
	v_pk_fma_f32 v[68:69], v[180:181], v[68:69], v[80:81] op_sel_hi:[1,0,1]
	s_waitcnt lgkmcnt(0)
	v_pk_mul_f32 v[80:81], v[64:65], v[68:69] op_sel:[1,1] op_sel_hi:[0,1] neg_hi:[1,0]
	s_nop 0
	v_pk_fma_f32 v[80:81], v[64:65], v[68:69], v[80:81] op_sel_hi:[1,0,1]
	v_pk_mul_f32 v[64:65], v[180:181], v[68:69] op_sel:[1,1] op_sel_hi:[0,1] neg_lo:[0,1]
	v_pk_fma_f32 v[64:65], v[180:181], v[68:69], v[64:65] op_sel_hi:[1,0,1]
	s_nop 0
	v_pk_mul_f32 v[68:69], v[66:67], v[64:65] op_sel:[1,1] op_sel_hi:[0,1] neg_hi:[1,0]
	s_nop 0
	v_pk_fma_f32 v[82:83], v[66:67], v[64:65], v[68:69] op_sel_hi:[1,0,1]
	v_pk_mul_f32 v[66:67], v[180:181], v[64:65] op_sel:[1,1] op_sel_hi:[0,1] neg_lo:[0,1]
	v_pk_fma_f32 v[68:69], v[180:181], v[64:65], v[66:67] op_sel_hi:[1,0,1]
	v_xad_u32 v63, v50, 12, v10
	v_lshl_add_u32 v63, v63, 3, 0
	v_add_u32_e32 v63, 0x800, v63
	ds_read2_b64 v[64:67], v63 offset0:128 offset1:144
	v_pk_mul_f32 v[84:85], v[180:181], v[68:69] op_sel:[1,1] op_sel_hi:[0,1] neg_lo:[0,1]
	v_pk_fma_f32 v[84:85], v[180:181], v[68:69], v[84:85] op_sel_hi:[1,0,1]
	s_waitcnt lgkmcnt(0)
	v_pk_mul_f32 v[86:87], v[64:65], v[68:69] op_sel:[1,1] op_sel_hi:[0,1] neg_hi:[1,0]
	v_pk_fma_f32 v[86:87], v[64:65], v[68:69], v[86:87] op_sel_hi:[1,0,1]
	v_pk_mul_f32 v[64:65], v[66:67], v[84:85] op_sel:[1,1] op_sel_hi:[0,1] neg_hi:[1,0]
	v_pk_fma_f32 v[88:89], v[66:67], v[84:85], v[64:65] op_sel_hi:[1,0,1]
	v_xad_u32 v64, v50, 13, v10
	v_lshl_add_u32 v64, v64, 3, 0
	v_add_u32_e32 v64, 0x800, v64
	ds_read2_b64 v[66:69], v64 offset0:160 offset1:176
	v_pk_mul_f32 v[90:91], v[180:181], v[84:85] op_sel:[1,1] op_sel_hi:[0,1] neg_lo:[0,1]
	v_pk_fma_f32 v[84:85], v[180:181], v[84:85], v[90:91] op_sel_hi:[1,0,1]
	s_waitcnt lgkmcnt(0)
	v_pk_mul_f32 v[90:91], v[66:67], v[84:85] op_sel:[1,1] op_sel_hi:[0,1] neg_hi:[1,0]
	s_nop 0
	v_pk_fma_f32 v[90:91], v[66:67], v[84:85], v[90:91] op_sel_hi:[1,0,1]
	v_pk_mul_f32 v[66:67], v[180:181], v[84:85] op_sel:[1,1] op_sel_hi:[0,1] neg_lo:[0,1]
	v_pk_fma_f32 v[66:67], v[180:181], v[84:85], v[66:67] op_sel_hi:[1,0,1]
	s_nop 0
	v_pk_mul_f32 v[84:85], v[68:69], v[66:67] op_sel:[1,1] op_sel_hi:[0,1] neg_hi:[1,0]
	s_nop 0
	v_pk_fma_f32 v[84:85], v[68:69], v[66:67], v[84:85] op_sel_hi:[1,0,1]
	v_pk_mul_f32 v[68:69], v[180:181], v[66:67] op_sel:[1,1] op_sel_hi:[0,1] neg_lo:[0,1]
	v_pk_fma_f32 v[92:93], v[180:181], v[66:67], v[68:69] op_sel_hi:[1,0,1]
	v_xad_u32 v65, v50, 14, v10
	v_lshl_add_u32 v65, v65, 3, 0
	v_add_u32_e32 v65, 0x800, v65
	ds_read2_b64 v[66:69], v65 offset0:192 offset1:208
	v_pk_mul_f32 v[94:95], v[180:181], v[92:93] op_sel:[1,1] op_sel_hi:[0,1] neg_lo:[0,1]
	v_xad_u32 v10, v50, 15, v10
	s_waitcnt lgkmcnt(0)
	v_pk_mul_f32 v[96:97], v[66:67], v[92:93] op_sel:[1,1] op_sel_hi:[0,1] neg_hi:[1,0]
	v_lshl_add_u32 v10, v10, 3, 0
	v_pk_fma_f32 v[96:97], v[66:67], v[92:93], v[96:97] op_sel_hi:[1,0,1]
	v_pk_fma_f32 v[92:93], v[180:181], v[92:93], v[94:95] op_sel_hi:[1,0,1]
	s_nop 0
	v_pk_mul_f32 v[66:67], v[68:69], v[92:93] op_sel:[1,1] op_sel_hi:[0,1] neg_hi:[1,0]
	v_add_u32_e32 v101, 0x800, v10
	v_pk_fma_f32 v[94:95], v[68:69], v[92:93], v[66:67] op_sel_hi:[1,0,1]
	ds_read2_b64 v[66:69], v101 offset0:224 offset1:240
	v_pk_mul_f32 v[98:99], v[180:181], v[92:93] op_sel:[1,1] op_sel_hi:[0,1] neg_lo:[0,1]
	v_pk_fma_f32 v[92:93], v[180:181], v[92:93], v[98:99] op_sel_hi:[1,0,1]
	s_waitcnt lgkmcnt(0)
	v_pk_mul_f32 v[98:99], v[66:67], v[92:93] op_sel:[1,1] op_sel_hi:[0,1] neg_hi:[1,0]
	s_nop 0
	v_pk_fma_f32 v[66:67], v[66:67], v[92:93], v[98:99] op_sel_hi:[1,0,1]
	v_pk_mul_f32 v[98:99], v[180:181], v[92:93] op_sel:[1,1] op_sel_hi:[0,1] neg_lo:[0,1]
	v_pk_fma_f32 v[20:21], v[180:181], v[92:93], v[98:99] op_sel_hi:[1,0,1]
	s_nop 0
	v_pk_mul_f32 v[92:93], v[68:69], v[20:21] op_sel:[1,1] op_sel_hi:[0,1] neg_hi:[1,0]
	s_nop 0
	v_pk_fma_f32 v[68:69], v[68:69], v[20:21], v[92:93] op_sel_hi:[1,0,1]
	v_pk_add_f32 v[104:105], v[16:17], v[52:53]
	v_pk_add_f32 v[16:17], v[16:17], v[52:53] neg_lo:[0,1] neg_hi:[0,1]
	v_pk_add_f32 v[52:53], v[18:19], v[70:71]
	v_pk_add_f32 v[18:19], v[18:19], v[70:71] neg_lo:[0,1] neg_hi:[0,1]
	v_mov_b32_e32 v92, v164
	v_mov_b32_e32 v20, v165
	v_mov_b32_e32 v98, v166
	v_mov_b32_e32 v10, v167
	v_mov_b32_e32 v100, v168
	v_mov_b32_e32 v50, v169
	v_mov_b32_e32 v102, v170
	v_mov_b32_e32 v21, v171
	v_pk_mul_f32 v[70:71], v[102:103], v[18:19] op_sel:[0,1] op_sel_hi:[0,0] neg_lo:[0,1]
	v_pk_fma_f32 v[18:19], v[92:93], v[18:19], v[70:71] op_sel_hi:[0,1,1]
	v_pk_add_f32 v[70:71], v[22:23], v[72:73]
	v_pk_add_f32 v[22:23], v[22:23], v[72:73] neg_lo:[0,1] neg_hi:[0,1]
	s_nop 0
	v_pk_mul_f32 v[72:73], v[50:51], v[22:23] op_sel:[0,1] op_sel_hi:[0,0] neg_lo:[0,1]
	v_pk_fma_f32 v[22:23], v[20:21], v[22:23], v[72:73] op_sel_hi:[0,1,1]
	v_pk_add_f32 v[72:73], v[24:25], v[74:75]
	v_pk_add_f32 v[24:25], v[24:25], v[74:75] neg_lo:[0,1] neg_hi:[0,1]
	s_nop 0
	v_pk_mul_f32 v[74:75], v[100:101], v[24:25] op_sel:[0,1] op_sel_hi:[0,0] neg_lo:[0,1]
	v_pk_fma_f32 v[24:25], v[98:99], v[24:25], v[74:75] op_sel_hi:[0,1,1]
	v_pk_add_f32 v[74:75], v[28:29], v[76:77]
	v_pk_add_f32 v[28:29], v[28:29], v[76:77] neg_lo:[0,1] neg_hi:[0,1]
	s_nop 0
	v_pk_mul_f32 v[76:77], v[10:11], v[28:29] op_sel:[0,1] op_sel_hi:[0,0] neg_lo:[0,1]
	v_pk_fma_f32 v[28:29], v[10:11], v[28:29], v[76:77] op_sel_hi:[0,1,1]
	v_pk_add_f32 v[76:77], v[26:27], v[78:79]
	v_pk_add_f32 v[26:27], v[26:27], v[78:79] neg_lo:[0,1] neg_hi:[0,1]
	s_nop 0
	v_pk_mul_f32 v[78:79], v[98:99], v[26:27] op_sel:[0,1] op_sel_hi:[0,0] neg_lo:[0,1]
	v_pk_fma_f32 v[26:27], v[100:101], v[26:27], v[78:79] op_sel_hi:[0,1,1]
	v_pk_add_f32 v[78:79], v[30:31], v[80:81]
	v_pk_add_f32 v[30:31], v[30:31], v[80:81] neg_lo:[0,1] neg_hi:[0,1]
	s_nop 0
	v_pk_mul_f32 v[80:81], v[20:21], v[30:31] op_sel:[0,1] op_sel_hi:[0,0] neg_lo:[0,1]
	v_pk_fma_f32 v[30:31], v[50:51], v[30:31], v[80:81] op_sel_hi:[0,1,1]
	v_pk_add_f32 v[80:81], v[32:33], v[82:83]
	v_pk_add_f32 v[32:33], v[32:33], v[82:83] neg_lo:[0,1] neg_hi:[0,1]
	s_nop 0
	v_pk_mul_f32 v[82:83], v[92:93], v[32:33] op_sel:[0,1] op_sel_hi:[0,0] neg_lo:[0,1]
	v_pk_fma_f32 v[32:33], v[102:103], v[32:33], v[82:83] op_sel_hi:[0,1,1]
	v_pk_add_f32 v[82:83], v[34:35], v[86:87]
	v_pk_add_f32 v[34:35], v[34:35], v[86:87] neg_lo:[0,1] neg_hi:[0,1]
	s_nop 0
	v_xor_b32_e32 v86, 0x80000000, v35
	v_mov_b32_e32 v87, v34
	v_pk_add_f32 v[34:35], v[36:37], v[88:89]
	v_pk_add_f32 v[36:37], v[36:37], v[88:89] neg_lo:[0,1] neg_hi:[0,1]
	s_nop 0
	v_pk_mul_f32 v[88:89], v[92:93], v[36:37] op_sel:[0,1] op_sel_hi:[0,0] neg_lo:[0,1]
	v_pk_fma_f32 v[36:37], v[102:103], v[36:37], v[88:89] op_sel_hi:[0,1,1] neg_lo:[1,0,0] neg_hi:[1,0,0]
	v_pk_add_f32 v[88:89], v[38:39], v[90:91]
	v_pk_add_f32 v[38:39], v[38:39], v[90:91] neg_lo:[0,1] neg_hi:[0,1]
	s_nop 0
	v_pk_mul_f32 v[90:91], v[20:21], v[38:39] op_sel:[0,1] op_sel_hi:[0,0] neg_lo:[0,1]
	v_pk_fma_f32 v[38:39], v[50:51], v[38:39], v[90:91] op_sel_hi:[0,1,1] neg_lo:[1,0,0] neg_hi:[1,0,0]
	v_pk_add_f32 v[90:91], v[40:41], v[84:85]
	v_pk_add_f32 v[40:41], v[40:41], v[84:85] neg_lo:[0,1] neg_hi:[0,1]
	s_nop 0
	v_pk_mul_f32 v[84:85], v[98:99], v[40:41] op_sel:[0,1] op_sel_hi:[0,0] neg_lo:[0,1]
	v_pk_fma_f32 v[40:41], v[100:101], v[40:41], v[84:85] op_sel_hi:[0,1,1] neg_lo:[1,0,0] neg_hi:[1,0,0]
	v_pk_add_f32 v[84:85], v[44:45], v[96:97]
	v_pk_add_f32 v[44:45], v[44:45], v[96:97] neg_lo:[0,1] neg_hi:[0,1]
	s_nop 0
	v_pk_mul_f32 v[96:97], v[10:11], v[44:45] op_sel:[0,1] op_sel_hi:[0,0] neg_lo:[0,1]
	v_pk_fma_f32 v[44:45], v[10:11], v[44:45], v[96:97] op_sel_hi:[0,1,1] neg_lo:[1,0,0] neg_hi:[1,0,0]
	v_pk_add_f32 v[96:97], v[42:43], v[94:95]
	v_pk_add_f32 v[42:43], v[42:43], v[94:95] neg_lo:[0,1] neg_hi:[0,1]
	s_nop 0
	v_pk_mul_f32 v[94:95], v[100:101], v[42:43] op_sel:[0,1] op_sel_hi:[0,0] neg_lo:[0,1]
	v_pk_fma_f32 v[42:43], v[98:99], v[42:43], v[94:95] op_sel_hi:[0,1,1] neg_lo:[1,0,0] neg_hi:[1,0,0]
	v_pk_add_f32 v[94:95], v[46:47], v[66:67]
	v_pk_add_f32 v[46:47], v[46:47], v[66:67] neg_lo:[0,1] neg_hi:[0,1]
	s_nop 0
	v_pk_mul_f32 v[66:67], v[50:51], v[46:47] op_sel:[0,1] op_sel_hi:[0,0] neg_lo:[0,1]
	v_pk_fma_f32 v[46:47], v[20:21], v[46:47], v[66:67] op_sel_hi:[0,1,1] neg_lo:[1,0,0] neg_hi:[1,0,0]
	v_pk_add_f32 v[66:67], v[48:49], v[68:69]
	v_pk_add_f32 v[48:49], v[48:49], v[68:69] neg_lo:[0,1] neg_hi:[0,1]
	s_nop 0
	v_pk_mul_f32 v[68:69], v[102:103], v[48:49] op_sel:[0,1] op_sel_hi:[0,0] neg_lo:[0,1]
	v_pk_fma_f32 v[48:49], v[92:93], v[48:49], v[68:69] op_sel_hi:[0,1,1] neg_lo:[1,0,0] neg_hi:[1,0,0]
	v_pk_add_f32 v[92:93], v[52:53], v[34:35]
	v_pk_add_f32 v[34:35], v[52:53], v[34:35] neg_lo:[0,1] neg_hi:[0,1]
	v_pk_add_f32 v[68:69], v[104:105], v[82:83]
	v_pk_mul_f32 v[52:53], v[50:51], v[34:35] op_sel:[0,1] op_sel_hi:[0,0] neg_lo:[0,1]
	v_pk_fma_f32 v[34:35], v[20:21], v[34:35], v[52:53] op_sel_hi:[0,1,1]
	v_pk_add_f32 v[52:53], v[70:71], v[88:89]
	v_pk_add_f32 v[70:71], v[70:71], v[88:89] neg_lo:[0,1] neg_hi:[0,1]
	v_pk_add_f32 v[82:83], v[104:105], v[82:83] neg_lo:[0,1] neg_hi:[0,1]
	v_pk_mul_f32 v[88:89], v[10:11], v[70:71] op_sel:[0,1] op_sel_hi:[0,0] neg_lo:[0,1]
	v_pk_fma_f32 v[70:71], v[10:11], v[70:71], v[88:89] op_sel_hi:[0,1,1]
	v_pk_add_f32 v[88:89], v[72:73], v[90:91]
	v_pk_add_f32 v[72:73], v[72:73], v[90:91] neg_lo:[0,1] neg_hi:[0,1]
	s_nop 0
	v_pk_mul_f32 v[90:91], v[20:21], v[72:73] op_sel:[0,1] op_sel_hi:[0,0] neg_lo:[0,1]
	v_pk_fma_f32 v[72:73], v[50:51], v[72:73], v[90:91] op_sel_hi:[0,1,1]
	v_pk_add_f32 v[90:91], v[74:75], v[84:85]
	v_pk_add_f32 v[74:75], v[74:75], v[84:85] neg_lo:[0,1] neg_hi:[0,1]
	s_nop 0
	v_xor_b32_e32 v84, 0x80000000, v75
	v_mov_b32_e32 v85, v74
	v_pk_add_f32 v[74:75], v[76:77], v[96:97]
	v_pk_add_f32 v[76:77], v[76:77], v[96:97] neg_lo:[0,1] neg_hi:[0,1]
	s_nop 0
	v_pk_mul_f32 v[96:97], v[20:21], v[76:77] op_sel:[0,1] op_sel_hi:[0,0] neg_lo:[0,1]
	v_pk_fma_f32 v[76:77], v[50:51], v[76:77], v[96:97] op_sel_hi:[0,1,1] neg_lo:[1,0,0] neg_hi:[1,0,0]
	v_pk_add_f32 v[96:97], v[78:79], v[94:95]
	v_pk_add_f32 v[78:79], v[78:79], v[94:95] neg_lo:[0,1] neg_hi:[0,1]
	s_nop 0
	v_pk_mul_f32 v[94:95], v[10:11], v[78:79] op_sel:[0,1] op_sel_hi:[0,0] neg_lo:[0,1]
	v_pk_fma_f32 v[78:79], v[10:11], v[78:79], v[94:95] op_sel_hi:[0,1,1] neg_lo:[1,0,0] neg_hi:[1,0,0]
	v_pk_add_f32 v[94:95], v[80:81], v[66:67]
	v_pk_add_f32 v[66:67], v[80:81], v[66:67] neg_lo:[0,1] neg_hi:[0,1]
	s_nop 0
	v_pk_mul_f32 v[80:81], v[50:51], v[66:67] op_sel:[0,1] op_sel_hi:[0,0] neg_lo:[0,1]
	v_pk_fma_f32 v[66:67], v[20:21], v[66:67], v[80:81] op_sel_hi:[0,1,1] neg_lo:[1,0,0] neg_hi:[1,0,0]
	v_pk_add_f32 v[80:81], v[68:69], v[90:91]
	v_pk_add_f32 v[68:69], v[68:69], v[90:91] neg_lo:[0,1] neg_hi:[0,1]
	v_pk_add_f32 v[90:91], v[92:93], v[74:75]
	v_pk_add_f32 v[74:75], v[92:93], v[74:75] neg_lo:[0,1] neg_hi:[0,1]
	s_nop 0
	v_pk_mul_f32 v[92:93], v[10:11], v[74:75] op_sel:[0,1] op_sel_hi:[0,0] neg_lo:[0,1]
	v_pk_fma_f32 v[74:75], v[10:11], v[74:75], v[92:93] op_sel_hi:[0,1,1]
	v_pk_add_f32 v[92:93], v[52:53], v[96:97]
	v_pk_add_f32 v[52:53], v[52:53], v[96:97] neg_lo:[0,1] neg_hi:[0,1]
	s_nop 0
	v_xor_b32_e32 v96, 0x80000000, v53
	v_mov_b32_e32 v97, v52
	v_pk_add_f32 v[52:53], v[88:89], v[94:95]
	v_pk_add_f32 v[88:89], v[88:89], v[94:95] neg_lo:[0,1] neg_hi:[0,1]
	s_nop 0
	v_pk_mul_f32 v[94:95], v[10:11], v[88:89] op_sel:[0,1] op_sel_hi:[0,0] neg_lo:[0,1]
	v_pk_fma_f32 v[88:89], v[10:11], v[88:89], v[94:95] op_sel_hi:[0,1,1] neg_lo:[1,0,0] neg_hi:[1,0,0]
	v_pk_add_f32 v[94:95], v[80:81], v[92:93]
	v_pk_add_f32 v[80:81], v[80:81], v[92:93] neg_lo:[0,1] neg_hi:[0,1]
	v_pk_add_f32 v[92:93], v[90:91], v[52:53]
	v_pk_add_f32 v[52:53], v[90:91], v[52:53] neg_lo:[0,1] neg_hi:[0,1]
	s_nop 0
	v_xor_b32_e32 v90, 0x80000000, v53
	v_mov_b32_e32 v91, v52
	v_pk_add_f32 v[52:53], v[94:95], v[92:93]
	v_pk_add_f32 v[92:93], v[94:95], v[92:93] neg_lo:[0,1] neg_hi:[0,1]
	v_pk_add_f32 v[94:95], v[80:81], v[90:91]
	v_pk_add_f32 v[80:81], v[80:81], v[90:91] neg_lo:[0,1] neg_hi:[0,1]
	v_pk_add_f32 v[90:91], v[68:69], v[96:97]
	v_pk_add_f32 v[68:69], v[68:69], v[96:97] neg_lo:[0,1] neg_hi:[0,1]
	v_pk_add_f32 v[96:97], v[74:75], v[88:89]
	v_pk_add_f32 v[74:75], v[74:75], v[88:89] neg_lo:[0,1] neg_hi:[0,1]
	s_nop 0
	v_xor_b32_e32 v88, 0x80000000, v75
	v_mov_b32_e32 v89, v74
	v_pk_add_f32 v[74:75], v[90:91], v[96:97]
	v_pk_add_f32 v[90:91], v[90:91], v[96:97] neg_lo:[0,1] neg_hi:[0,1]
	v_pk_add_f32 v[96:97], v[68:69], v[88:89]
	v_pk_add_f32 v[68:69], v[68:69], v[88:89] neg_lo:[0,1] neg_hi:[0,1]
	v_pk_add_f32 v[88:89], v[82:83], v[84:85]
	v_pk_add_f32 v[82:83], v[82:83], v[84:85] neg_lo:[0,1] neg_hi:[0,1]
	v_pk_add_f32 v[84:85], v[34:35], v[76:77]
	v_pk_add_f32 v[34:35], v[34:35], v[76:77] neg_lo:[0,1] neg_hi:[0,1]
	s_nop 0
	v_pk_mul_f32 v[76:77], v[10:11], v[34:35] op_sel:[0,1] op_sel_hi:[0,0] neg_lo:[0,1]
	v_pk_fma_f32 v[34:35], v[10:11], v[34:35], v[76:77] op_sel_hi:[0,1,1]
	v_pk_add_f32 v[76:77], v[70:71], v[78:79]
	v_pk_add_f32 v[70:71], v[70:71], v[78:79] neg_lo:[0,1] neg_hi:[0,1]
	s_nop 0
	v_xor_b32_e32 v78, 0x80000000, v71
	v_mov_b32_e32 v79, v70
	v_pk_add_f32 v[70:71], v[72:73], v[66:67]
	v_pk_add_f32 v[66:67], v[72:73], v[66:67] neg_lo:[0,1] neg_hi:[0,1]
	s_nop 0
	v_pk_mul_f32 v[72:73], v[10:11], v[66:67] op_sel:[0,1] op_sel_hi:[0,0] neg_lo:[0,1]
	v_pk_fma_f32 v[66:67], v[10:11], v[66:67], v[72:73] op_sel_hi:[0,1,1] neg_lo:[1,0,0] neg_hi:[1,0,0]
	v_pk_add_f32 v[72:73], v[88:89], v[76:77]
	v_pk_add_f32 v[76:77], v[88:89], v[76:77] neg_lo:[0,1] neg_hi:[0,1]
	v_pk_add_f32 v[88:89], v[84:85], v[70:71]
	v_pk_add_f32 v[70:71], v[84:85], v[70:71] neg_lo:[0,1] neg_hi:[0,1]
	s_nop 0
	v_xor_b32_e32 v84, 0x80000000, v71
	v_mov_b32_e32 v85, v70
	v_pk_add_f32 v[70:71], v[72:73], v[88:89]
	v_pk_add_f32 v[72:73], v[72:73], v[88:89] neg_lo:[0,1] neg_hi:[0,1]
	v_pk_add_f32 v[88:89], v[76:77], v[84:85]
	v_pk_add_f32 v[76:77], v[76:77], v[84:85] neg_lo:[0,1] neg_hi:[0,1]
	v_pk_add_f32 v[84:85], v[82:83], v[78:79]
	v_pk_add_f32 v[78:79], v[82:83], v[78:79] neg_lo:[0,1] neg_hi:[0,1]
	v_pk_add_f32 v[82:83], v[34:35], v[66:67]
	v_pk_add_f32 v[34:35], v[34:35], v[66:67] neg_lo:[0,1] neg_hi:[0,1]
	s_nop 0
	v_xor_b32_e32 v66, 0x80000000, v35
	v_mov_b32_e32 v67, v34
	v_pk_add_f32 v[34:35], v[84:85], v[82:83]
	v_pk_add_f32 v[82:83], v[84:85], v[82:83] neg_lo:[0,1] neg_hi:[0,1]
	v_pk_add_f32 v[84:85], v[78:79], v[66:67]
	v_pk_add_f32 v[66:67], v[78:79], v[66:67] neg_lo:[0,1] neg_hi:[0,1]
	v_pk_add_f32 v[78:79], v[16:17], v[86:87]
	v_pk_add_f32 v[16:17], v[16:17], v[86:87] neg_lo:[0,1] neg_hi:[0,1]
	v_pk_add_f32 v[86:87], v[18:19], v[36:37]
	v_pk_add_f32 v[18:19], v[18:19], v[36:37] neg_lo:[0,1] neg_hi:[0,1]
	s_nop 0
	v_pk_mul_f32 v[36:37], v[50:51], v[18:19] op_sel:[0,1] op_sel_hi:[0,0] neg_lo:[0,1]
	v_pk_fma_f32 v[18:19], v[20:21], v[18:19], v[36:37] op_sel_hi:[0,1,1]
	v_pk_add_f32 v[36:37], v[22:23], v[38:39]
	v_pk_add_f32 v[22:23], v[22:23], v[38:39] neg_lo:[0,1] neg_hi:[0,1]
	s_nop 0
	v_pk_mul_f32 v[38:39], v[10:11], v[22:23] op_sel:[0,1] op_sel_hi:[0,0] neg_lo:[0,1]
	v_pk_fma_f32 v[22:23], v[10:11], v[22:23], v[38:39] op_sel_hi:[0,1,1]
	v_pk_add_f32 v[38:39], v[24:25], v[40:41]
	v_pk_add_f32 v[24:25], v[24:25], v[40:41] neg_lo:[0,1] neg_hi:[0,1]
	s_nop 0
	v_pk_mul_f32 v[40:41], v[20:21], v[24:25] op_sel:[0,1] op_sel_hi:[0,0] neg_lo:[0,1]
	v_pk_fma_f32 v[24:25], v[50:51], v[24:25], v[40:41] op_sel_hi:[0,1,1]
	v_pk_add_f32 v[40:41], v[28:29], v[44:45]
	v_pk_add_f32 v[28:29], v[28:29], v[44:45] neg_lo:[0,1] neg_hi:[0,1]
	s_nop 0
	v_xor_b32_e32 v44, 0x80000000, v29
	v_mov_b32_e32 v45, v28
	v_pk_add_f32 v[28:29], v[26:27], v[42:43]
	v_pk_add_f32 v[26:27], v[26:27], v[42:43] neg_lo:[0,1] neg_hi:[0,1]
	s_nop 0
	v_pk_mul_f32 v[42:43], v[20:21], v[26:27] op_sel:[0,1] op_sel_hi:[0,0] neg_lo:[0,1]
	v_pk_fma_f32 v[26:27], v[50:51], v[26:27], v[42:43] op_sel_hi:[0,1,1] neg_lo:[1,0,0] neg_hi:[1,0,0]
	v_pk_add_f32 v[42:43], v[30:31], v[46:47]
	v_pk_add_f32 v[30:31], v[30:31], v[46:47] neg_lo:[0,1] neg_hi:[0,1]
	s_nop 0
	v_pk_mul_f32 v[46:47], v[10:11], v[30:31] op_sel:[0,1] op_sel_hi:[0,0] neg_lo:[0,1]
	v_pk_fma_f32 v[30:31], v[10:11], v[30:31], v[46:47] op_sel_hi:[0,1,1] neg_lo:[1,0,0] neg_hi:[1,0,0]
	v_pk_add_f32 v[46:47], v[32:33], v[48:49]
	v_pk_add_f32 v[32:33], v[32:33], v[48:49] neg_lo:[0,1] neg_hi:[0,1]
	s_nop 0
	v_pk_mul_f32 v[48:49], v[50:51], v[32:33] op_sel:[0,1] op_sel_hi:[0,0] neg_lo:[0,1]
	v_pk_fma_f32 v[20:21], v[20:21], v[32:33], v[48:49] op_sel_hi:[0,1,1] neg_lo:[1,0,0] neg_hi:[1,0,0]
	v_pk_add_f32 v[48:49], v[86:87], v[28:29]
	v_pk_add_f32 v[28:29], v[86:87], v[28:29] neg_lo:[0,1] neg_hi:[0,1]
	v_pk_add_f32 v[32:33], v[78:79], v[40:41]
	v_pk_add_f32 v[40:41], v[78:79], v[40:41] neg_lo:[0,1] neg_hi:[0,1]
	v_pk_mul_f32 v[78:79], v[10:11], v[28:29] op_sel:[0,1] op_sel_hi:[0,0] neg_lo:[0,1]
	v_pk_fma_f32 v[28:29], v[10:11], v[28:29], v[78:79] op_sel_hi:[0,1,1]
	v_pk_add_f32 v[78:79], v[36:37], v[42:43]
	v_pk_add_f32 v[36:37], v[36:37], v[42:43] neg_lo:[0,1] neg_hi:[0,1]
	s_nop 0
	v_xor_b32_e32 v42, 0x80000000, v37
	v_mov_b32_e32 v43, v36
	v_pk_add_f32 v[36:37], v[38:39], v[46:47]
	v_pk_add_f32 v[38:39], v[38:39], v[46:47] neg_lo:[0,1] neg_hi:[0,1]
	s_nop 0
	v_pk_mul_f32 v[46:47], v[10:11], v[38:39] op_sel:[0,1] op_sel_hi:[0,0] neg_lo:[0,1]
	v_pk_fma_f32 v[38:39], v[10:11], v[38:39], v[46:47] op_sel_hi:[0,1,1] neg_lo:[1,0,0] neg_hi:[1,0,0]
	v_pk_add_f32 v[46:47], v[32:33], v[78:79]
	v_pk_add_f32 v[32:33], v[32:33], v[78:79] neg_lo:[0,1] neg_hi:[0,1]
	v_pk_add_f32 v[78:79], v[48:49], v[36:37]
	v_pk_add_f32 v[36:37], v[48:49], v[36:37] neg_lo:[0,1] neg_hi:[0,1]
	s_nop 0
	v_pk_add_f32 v[86:87], v[32:33], v[36:37] op_sel:[0,1] op_sel_hi:[1,0] neg_lo:[0,1]
	v_pk_add_f32 v[32:33], v[32:33], v[36:37] op_sel:[0,1] op_sel_hi:[1,0] neg_hi:[0,1]
	v_pk_add_f32 v[48:49], v[40:41], v[42:43]
	v_pk_add_f32 v[40:41], v[40:41], v[42:43] neg_lo:[0,1] neg_hi:[0,1]
	v_pk_add_f32 v[42:43], v[28:29], v[38:39]
	v_pk_add_f32 v[28:29], v[28:29], v[38:39] neg_lo:[0,1] neg_hi:[0,1]
	v_pk_add_f32 v[36:37], v[46:47], v[78:79] neg_lo:[0,1] neg_hi:[0,1]
	v_xor_b32_e32 v38, 0x80000000, v29
	v_mov_b32_e32 v39, v28
	v_pk_add_f32 v[28:29], v[48:49], v[42:43]
	v_pk_add_f32 v[42:43], v[48:49], v[42:43] neg_lo:[0,1] neg_hi:[0,1]
	v_pk_add_f32 v[48:49], v[40:41], v[38:39]
	v_pk_add_f32 v[38:39], v[40:41], v[38:39] neg_lo:[0,1] neg_hi:[0,1]
	v_pk_add_f32 v[40:41], v[16:17], v[44:45]
	v_pk_add_f32 v[16:17], v[16:17], v[44:45] neg_lo:[0,1] neg_hi:[0,1]
	v_pk_add_f32 v[44:45], v[18:19], v[26:27]
	v_pk_add_f32 v[18:19], v[18:19], v[26:27] neg_lo:[0,1] neg_hi:[0,1]
	s_nop 0
	v_pk_mul_f32 v[26:27], v[10:11], v[18:19] op_sel:[0,1] op_sel_hi:[0,0] neg_lo:[0,1]
	v_pk_fma_f32 v[18:19], v[10:11], v[18:19], v[26:27] op_sel_hi:[0,1,1]
	v_pk_add_f32 v[26:27], v[22:23], v[30:31]
	v_pk_add_f32 v[22:23], v[22:23], v[30:31] neg_lo:[0,1] neg_hi:[0,1]
	s_nop 0
	v_xor_b32_e32 v30, 0x80000000, v23
	v_mov_b32_e32 v31, v22
	v_pk_add_f32 v[22:23], v[24:25], v[20:21]
	v_pk_add_f32 v[20:21], v[24:25], v[20:21] neg_lo:[0,1] neg_hi:[0,1]
	s_nop 0
	v_pk_mul_f32 v[24:25], v[10:11], v[20:21] op_sel:[0,1] op_sel_hi:[0,0] neg_lo:[0,1]
	v_pk_fma_f32 v[20:21], v[10:11], v[20:21], v[24:25] op_sel_hi:[0,1,1] neg_lo:[1,0,0] neg_hi:[1,0,0]
	v_pk_add_f32 v[24:25], v[40:41], v[26:27]
	v_pk_add_f32 v[26:27], v[40:41], v[26:27] neg_lo:[0,1] neg_hi:[0,1]
	v_pk_add_f32 v[40:41], v[44:45], v[22:23]
	v_pk_add_f32 v[22:23], v[44:45], v[22:23] neg_lo:[0,1] neg_hi:[0,1]
	s_nop 0
	v_xor_b32_e32 v44, 0x80000000, v23
	v_mov_b32_e32 v45, v22
	v_pk_add_f32 v[22:23], v[24:25], v[40:41]
	v_pk_add_f32 v[24:25], v[24:25], v[40:41] neg_lo:[0,1] neg_hi:[0,1]
	v_pk_add_f32 v[40:41], v[26:27], v[44:45]
	v_pk_add_f32 v[26:27], v[26:27], v[44:45] neg_lo:[0,1] neg_hi:[0,1]
	v_pk_add_f32 v[44:45], v[16:17], v[30:31]
	v_pk_add_f32 v[16:17], v[16:17], v[30:31] neg_lo:[0,1] neg_hi:[0,1]
	v_pk_add_f32 v[30:31], v[18:19], v[20:21]
	v_pk_add_f32 v[18:19], v[18:19], v[20:21] neg_lo:[0,1] neg_hi:[0,1]
	s_nop 0
	v_xor_b32_e32 v20, 0x80000000, v19
	v_mov_b32_e32 v21, v18
	v_pk_add_f32 v[18:19], v[44:45], v[30:31]
	v_pk_add_f32 v[30:31], v[44:45], v[30:31] neg_lo:[0,1] neg_hi:[0,1]
	v_pk_add_f32 v[44:45], v[16:17], v[20:21]
	v_pk_add_f32 v[16:17], v[16:17], v[20:21] neg_lo:[0,1] neg_hi:[0,1]
	v_pk_add_f32 v[20:21], v[46:47], v[78:79]
	ds_write2_b64 v13, v[52:53], v[20:21] offset1:16
	ds_write2_b64 v15, v[70:71], v[22:23] offset0:32 offset1:48
	ds_write2_b64 v51, v[74:75], v[28:29] offset0:64 offset1:80
	ds_write2_b64 v54, v[34:35], v[18:19] offset0:96 offset1:112
	ds_write2_b64 v55, v[94:95], v[86:87] offset0:128 offset1:144
	ds_write2_b64 v56, v[88:89], v[40:41] offset0:160 offset1:176
	ds_write2_b64 v57, v[96:97], v[48:49] offset0:192 offset1:208
	ds_write2_b64 v58, v[84:85], v[44:45] offset0:224 offset1:240
	ds_write2_b64 v59, v[92:93], v[36:37] offset1:16
	ds_write2_b64 v60, v[72:73], v[24:25] offset0:32 offset1:48
	ds_write2_b64 v61, v[90:91], v[42:43] offset0:64 offset1:80
	ds_write2_b64 v62, v[82:83], v[30:31] offset0:96 offset1:112
	ds_write2_b64 v63, v[80:81], v[32:33] offset0:128 offset1:144
	ds_write2_b64 v64, v[76:77], v[26:27] offset0:160 offset1:176
	ds_write2_b64 v65, v[68:69], v[38:39] offset0:192 offset1:208
	ds_write2_b64 v101, v[66:67], v[16:17] offset0:224 offset1:240
	v_mov_b32_e32 v10, v173
	s_waitcnt lgkmcnt(0)
	s_barrier
	v_mov_b32_e32 v58, v178
	v_mov_b32_e32 v59, v179
	v_lshl_add_u32 v10, v10, 3, 0
	ds_read_b64 v[34:35], v10
	ds_read_b64 v[36:37], v10 offset:4224
	ds_read_b64 v[38:39], v10 offset:8448
	ds_read_b64 v[40:41], v10 offset:12672
	ds_read_b64 v[42:43], v10 offset:16896
	ds_read_b64 v[44:45], v10 offset:21120
	ds_read_b64 v[50:51], v10 offset:25344
	ds_read_b64 v[52:53], v10 offset:29568
	ds_read_b64 v[54:55], v10 offset:33792
	ds_read_b64 v[56:57], v10 offset:38016
	ds_read_b64 v[64:65], v10 offset:42240
	ds_read_b64 v[74:75], v10 offset:46464
	ds_read_b64 v[76:77], v10 offset:50688
	ds_read_b64 v[78:79], v10 offset:54912
	ds_read_b64 v[80:81], v10 offset:59136
	ds_read_b64 v[82:83], v10 offset:63360
	v_add_u32_e32 v13, 0x10800, v10
	v_add_u32_e32 v15, 0x11880, v10
	v_add_u32_e32 v16, 0x12900, v10
	v_add_u32_e32 v17, 0x13980, v10
	ds_read_b64 v[84:85], v13
	ds_read_b64 v[86:87], v15
	ds_read_b64 v[88:89], v16
	ds_read_b64 v[92:93], v17
	v_add_u32_e32 v13, 0x14a00, v10
	v_add_u32_e32 v15, 0x15a80, v10
	v_add_u32_e32 v16, 0x16b00, v10
	v_add_u32_e32 v17, 0x17b80, v10
	ds_read_b64 v[96:97], v13
	ds_read_b64 v[98:99], v15
	ds_read_b64 v[94:95], v16
	ds_read_b64 v[90:91], v17
	v_add_u32_e32 v13, 0x18c00, v10
	v_add_u32_e32 v15, 0x19c80, v10
	v_add_u32_e32 v16, 0x1ad00, v10
	v_add_u32_e32 v17, 0x1bd80, v10
	ds_read_b64 v[72:73], v13
	ds_read_b64 v[70:71], v15
	ds_read_b64 v[68:69], v16
	ds_read_b64 v[66:67], v17
	v_add_u32_e32 v13, 0x1ce00, v10
	v_add_u32_e32 v15, 0x1de80, v10
	v_add_u32_e32 v16, 0x1ef00, v10
	v_add_u32_e32 v10, 0x1ff80, v10
	ds_read_b64 v[62:63], v13
	ds_read_b64 v[60:61], v15
	ds_read_b64 v[100:101], v16
	ds_read_b64 v[102:103], v10
	s_mov_b32 s43, s95
	s_lshl_b64 s[0:1], s[42:43], 2
	v_readlane_b32 s2, v251, 46
	s_add_u32 s0, s2, s0
	v_readlane_b32 s2, v251, 48
	v_readlane_b32 s6, v251, 52
	v_mov_b32_e32 v24, v164
	v_mov_b32_e32 v32, v165
	v_mov_b32_e32 v28, v166
	v_mov_b32_e32 v46, v167
	v_mov_b32_e32 v48, v168
	v_mov_b32_e32 v30, v169
	v_mov_b32_e32 v26, v170
	v_mov_b32_e32 v16, v183
	v_mov_b32_e32 v19, v184
	s_addc_u32 s1, s2, s1
	v_readlane_b32 s7, v251, 53
	s_waitcnt lgkmcnt(0)
	s_barrier
	global_load_dword v13, v11, s[0:1]
	s_and_b64 s[0:1], s[6:7], exec
	s_movk_i32 s0, 0x800
	s_cselect_b32 s2, 0x400, s0
	v_readlane_b32 s24, v251, 50
	s_add_i32 s4, s2, s24
	s_mul_i32 s0, s4, 0x8200
	v_readlane_b32 s3, v251, 18
	s_mul_hi_i32 s1, s4, 0x8200
	s_add_u32 s0, s3, s0
	v_readlane_b32 s3, v251, 20
	s_addc_u32 s1, s3, s1
	s_lshl_b32 s2, s2, 2
	v_mov_b32_e32 v10, s2
	v_readlane_b32 s2, v251, 42
	v_readlane_b32 s3, v251, 43
	v_readlane_b32 s8, v250, 23
	v_readlane_b32 s9, v250, 24
	v_ashrrev_i32_e32 v15, 31, v14
	v_lshl_add_u64 v[22:23], v[14:15], 2, s[70:71]
	v_readlane_b32 s22, v250, 37
	global_load_dword v197, v10, s[2:3]
	s_add_i32 s2, s4, 0xc00
	s_ashr_i32 s3, s2, 31
	s_lshl_b64 s[2:3], s[2:3], 2
	s_add_u32 s2, s8, s2
	s_addc_u32 s3, s9, s3
	global_load_dword v198, v11, s[2:3]
	s_add_i32 s2, s4, 0x1800
	s_ashr_i32 s3, s2, 31
	s_lshl_b64 s[2:3], s[2:3], 2
	s_add_u32 s2, s8, s2
	s_addc_u32 s3, s9, s3
	global_load_dword v199, v11, s[2:3]
	v_readlane_b32 s2, v251, 40
	v_readlane_b32 s3, v251, 41
	v_cmp_lt_i32_e32 vcc, 0, v14
	v_mov_b32_e32 v17, 0
	v_lshl_add_u64 v[20:21], v[14:15], 1, s[0:1]
	v_mov_b32_e32 v18, 0
	v_readlane_b32 s25, v251, 51
	global_load_dword v200, v10, s[2:3]
	v_readlane_b32 s10, v250, 25
	v_lshlrev_b32_e32 v241, 1, v14
	v_lshlrev_b32_e32 v242, 2, v14
	v_add_u32_e32 v242, 0x1000, v242
	global_load_dword v190, v242, s[70:71] offset:-4096
	global_load_ushort v202, v241, s[0:1] offset:-2
	global_load_ushort v203, v241, s[0:1]
	global_load_ushort v204, v241, s[0:1] offset:2
	global_load_dword v205, v242, s[64:65] offset:-4096
	global_load_dword v206, v242, s[70:71] offset:-2048
	global_load_ushort v207, v241, s[0:1] offset:1022
	global_load_ushort v208, v241, s[0:1] offset:1024
	global_load_ushort v209, v241, s[0:1] offset:1026
	global_load_dword v210, v242, s[64:65] offset:-2048
	global_load_dword v211, v242, s[70:71]
	global_load_ushort v212, v241, s[0:1] offset:2046
	global_load_ushort v213, v241, s[0:1] offset:2048
	global_load_ushort v214, v241, s[0:1] offset:2050
	global_load_dword v215, v242, s[64:65]
	global_load_dword v216, v242, s[70:71] offset:2048
	global_load_ushort v217, v241, s[0:1] offset:3070
	global_load_ushort v218, v241, s[0:1] offset:3072
	global_load_ushort v219, v241, s[0:1] offset:3074
	global_load_dword v220, v242, s[64:65] offset:2048
	v_lshlrev_b32_e32 v241, 1, v14
	v_add_u32_e32 v241, 0x1000, v241
	v_lshlrev_b32_e32 v242, 2, v14
	v_add_u32_e32 v242, 0x3000, v242
	global_load_dword v221, v242, s[70:71] offset:-4096
	global_load_ushort v222, v241, s[0:1] offset:-2
	global_load_ushort v223, v241, s[0:1]
	global_load_ushort v224, v241, s[0:1] offset:2
	global_load_dword v225, v242, s[64:65] offset:-4096
	global_load_dword v226, v242, s[70:71] offset:-2048
	global_load_ushort v227, v241, s[0:1] offset:1022
	global_load_ushort v228, v241, s[0:1] offset:1024
	global_load_ushort v229, v241, s[0:1] offset:1026
	global_load_dword v230, v242, s[64:65] offset:-2048
	global_load_dword v231, v242, s[70:71]
	global_load_ushort v232, v241, s[0:1] offset:2046
	global_load_ushort v233, v241, s[0:1] offset:2048
	global_load_ushort v234, v241, s[0:1] offset:2050
	global_load_dword v235, v242, s[64:65]
	global_load_dword v236, v242, s[70:71] offset:2048
	global_load_ushort v237, v241, s[0:1] offset:3070
	global_load_ushort v238, v241, s[0:1] offset:3072
	global_load_ushort v239, v241, s[0:1] offset:3074
	global_load_dword v240, v242, s[64:65] offset:2048
	s_waitcnt vmcnt(20)
	v_mov_b32_e32 v10, v190
	v_readlane_b32 s11, v250, 26
	v_readlane_b32 s12, v250, 27
	v_readlane_b32 s13, v250, 28
	v_readlane_b32 s14, v250, 29
	v_readlane_b32 s15, v250, 30
	v_readlane_b32 s16, v250, 31
	v_readlane_b32 s17, v250, 32
	v_readlane_b32 s18, v250, 33
	v_readlane_b32 s19, v250, 34
	v_readlane_b32 s20, v250, 35
	v_readlane_b32 s21, v250, 36
	v_readlane_b32 s23, v250, 38
	s_and_saveexec_b64 s[2:3], vcc
	s_movk_i32 s22, 0x3fff
	s_cbranch_execz .LBB0_636
	v_mov_b32_e32 v18, v202
	s_nop 0
	v_lshlrev_b32_e32 v18, 16, v18

.LBB0_642:
	v_mov_b32_e32 v25, v206
	v_cmp_lt_i32_e32 vcc, s23, v14
	v_mov_b32_e32 v15, 0
	v_mov_b32_e32 v10, 0
	s_and_saveexec_b64 s[4:5], vcc
	s_cbranch_execz .LBB0_644
	v_mov_b32_e32 v10, v207
	s_nop 0
	v_lshlrev_b32_e32 v10, 16, v10

.LBB0_650:
	v_add_co_u32_e32 v8, vcc, 0x1000, v22
	v_mov_b32_e32 v15, 0
	s_nop 0
	v_addc_co_u32_e32 v9, vcc, 0, v23, vcc
	v_mov_b32_e32 v120, v211
	v_cmp_lt_i32_e32 vcc, s48, v14
	v_mov_b32_e32 v10, 0
	s_and_saveexec_b64 s[2:3], vcc
	s_cbranch_execz .LBB0_652
	v_mov_b32_e32 v8, v212
	s_nop 0
	v_lshlrev_b32_e32 v10, 16, v8

.LBB0_658:
	v_add_co_u32_e32 v74, vcc, 0x1000, v22
	v_mov_b32_e32 v15, 0
	s_nop 0
	v_addc_co_u32_e32 v75, vcc, 0, v23, vcc
	v_mov_b32_e32 v88, v216
	v_cmp_lt_i32_e32 vcc, s49, v14
	v_mov_b32_e32 v10, 0
	s_and_saveexec_b64 s[2:3], vcc
	s_cbranch_execz .LBB0_660
	v_mov_b32_e32 v10, v217
	s_nop 0
	v_lshlrev_b32_e32 v10, 16, v10

.LBB0_666:
	v_add_co_u32_e32 v86, vcc, 0x2000, v22
	v_add_u32_e32 v138, 0x800, v14
	s_nop 0
	v_addc_co_u32_e32 v87, vcc, 0, v23, vcc
	v_lshlrev_b32_e32 v241, 1, v14
	v_add_u32_e32 v241, 0x2000, v241
	v_lshlrev_b32_e32 v242, 2, v14
	v_add_u32_e32 v242, 0x5000, v242
	global_load_dword v190, v242, s[70:71] offset:-4096
	global_load_ushort v202, v241, s[0:1] offset:-2
	global_load_ushort v203, v241, s[0:1]
	global_load_ushort v204, v241, s[0:1] offset:2
	global_load_dword v205, v242, s[64:65] offset:-4096
	global_load_dword v206, v242, s[70:71] offset:-2048
	global_load_ushort v207, v241, s[0:1] offset:1022
	global_load_ushort v208, v241, s[0:1] offset:1024
	global_load_ushort v209, v241, s[0:1] offset:1026
	global_load_dword v210, v242, s[64:65] offset:-2048
	global_load_dword v211, v242, s[70:71]
	global_load_ushort v212, v241, s[0:1] offset:2046
	global_load_ushort v213, v241, s[0:1] offset:2048
	global_load_ushort v214, v241, s[0:1] offset:2050
	global_load_dword v215, v242, s[64:65]
	global_load_dword v216, v242, s[70:71] offset:2048
	global_load_ushort v217, v241, s[0:1] offset:3070
	global_load_ushort v218, v241, s[0:1] offset:3072
	global_load_ushort v219, v241, s[0:1] offset:3074
	global_load_dword v220, v242, s[64:65] offset:2048
	s_waitcnt vmcnt(20)
	v_mov_b32_e32 v10, v221
	v_ashrrev_i32_e32 v139, 31, v138
	v_cmp_lt_i32_e32 vcc, s50, v14
	v_mov_b32_e32 v15, 0
	v_mov_b32_e32 v140, 0
	s_and_saveexec_b64 s[2:3], vcc
	s_cbranch_execz .LBB0_668
	v_mov_b32_e32 v86, v222
	s_nop 0
	v_lshlrev_b32_e32 v140, 16, v86
.LBB0_668:
	s_or_b64 exec, exec, s[2:3]
	v_add_co_u32_e32 v86, vcc, 0x1000, v20
	s_movk_i32 s2, 0x37ff
	s_nop 0
	v_addc_co_u32_e32 v87, vcc, 0, v21, vcc
	v_mov_b32_e32 v141, v223
	v_cmp_gt_i32_e32 vcc, s2, v14
	s_and_saveexec_b64 s[2:3], vcc
	s_cbranch_execz .LBB0_670
	s_mov_b64 s[6:7], 0x1000
	v_mov_b32_e32 v15, v224
	s_nop 0
	v_lshlrev_b32_e32 v15, 16, v15

.LBB0_674:
	v_add_co_u32_e32 v38, vcc, 0x2000, v22
	v_add_u32_e32 v42, 0xa00, v14
	s_nop 0
	v_addc_co_u32_e32 v39, vcc, 0, v23, vcc
	v_mov_b32_e32 v10, v226
	v_ashrrev_i32_e32 v43, 31, v42
	v_cmp_lt_i32_e32 vcc, s51, v14
	v_mov_b32_e32 v15, 0
	v_mov_b32_e32 v44, 0
	s_and_saveexec_b64 s[2:3], vcc
	s_cbranch_execz .LBB0_676
	v_mov_b32_e32 v38, v227
	s_nop 0
	v_lshlrev_b32_e32 v44, 16, v38
.LBB0_676:
	s_or_b64 exec, exec, s[2:3]
	v_add_co_u32_e32 v38, vcc, 0x1000, v20
	s_movk_i32 s2, 0x35ff
	s_nop 0
	v_addc_co_u32_e32 v39, vcc, 0, v21, vcc
	v_mov_b32_e32 v45, v228
	v_cmp_gt_i32_e32 vcc, s2, v14
	s_and_saveexec_b64 s[2:3], vcc
	s_cbranch_execz .LBB0_678
	s_mov_b64 s[6:7], 0x1400
	v_mov_b32_e32 v15, v229
	s_nop 0
	v_lshlrev_b32_e32 v15, 16, v15

.LBB0_682:
	v_add_co_u32_e32 v42, vcc, 0x3000, v22
	v_add_u32_e32 v116, 0xc00, v14
	s_nop 0
	v_addc_co_u32_e32 v43, vcc, 0, v23, vcc
	v_mov_b32_e32 v10, v231
	v_ashrrev_i32_e32 v117, 31, v116
	v_cmp_lt_i32_e32 vcc, s57, v14
	v_mov_b32_e32 v15, 0
	v_mov_b32_e32 v122, 0
	s_and_saveexec_b64 s[2:3], vcc
	s_cbranch_execz .LBB0_684
	v_mov_b32_e32 v42, v232
	s_nop 0
	v_lshlrev_b32_e32 v122, 16, v42
.LBB0_684:
	s_or_b64 exec, exec, s[2:3]
	v_add_co_u32_e32 v42, vcc, 0x1000, v20
	s_movk_i32 s2, 0x33ff
	s_nop 0
	v_addc_co_u32_e32 v43, vcc, 0, v21, vcc
	v_mov_b32_e32 v123, v233
	v_cmp_gt_i32_e32 vcc, s2, v14
	s_and_saveexec_b64 s[2:3], vcc
	s_cbranch_execz .LBB0_686
	s_mov_b64 s[6:7], 0x1800
	v_mov_b32_e32 v15, v234
	s_nop 0
	v_lshlrev_b32_e32 v15, 16, v15

.LBB0_690:
	v_add_co_u32_e32 v106, vcc, 0x3000, v22
	v_add_u32_e32 v116, 0xe00, v14
	s_nop 0
	v_addc_co_u32_e32 v107, vcc, 0, v23, vcc
	v_mov_b32_e32 v10, v236
	v_ashrrev_i32_e32 v117, 31, v116
	v_cmp_lt_i32_e32 vcc, s58, v14
	v_mov_b32_e32 v15, 0
	v_mov_b32_e32 v122, 0
	s_and_saveexec_b64 s[2:3], vcc
	s_cbranch_execz .LBB0_692
	v_mov_b32_e32 v106, v237
	s_nop 0
	v_lshlrev_b32_e32 v122, 16, v106
.LBB0_692:
	s_or_b64 exec, exec, s[2:3]
	v_add_co_u32_e32 v106, vcc, 0x1000, v20
	s_movk_i32 s2, 0x31ff
	s_nop 0
	v_addc_co_u32_e32 v107, vcc, 0, v21, vcc
	v_mov_b32_e32 v123, v238
	v_cmp_gt_i32_e32 vcc, s2, v14
	s_and_saveexec_b64 s[2:3], vcc
	s_cbranch_execz .LBB0_694
	s_mov_b64 s[6:7], 0x1c00
	v_mov_b32_e32 v15, v239
	s_nop 0
	v_lshlrev_b32_e32 v15, 16, v15

.LBB0_698:
	v_add_co_u32_e32 v114, vcc, 0x4000, v22
	v_mov_b32_e32 v15, 0
	s_nop 0
	v_addc_co_u32_e32 v115, vcc, 0, v23, vcc
	v_lshlrev_b32_e32 v241, 1, v14
	v_add_u32_e32 v241, 0x3000, v241
	v_lshlrev_b32_e32 v242, 2, v14
	v_add_u32_e32 v242, 0x7000, v242
	global_load_dword v221, v242, s[70:71] offset:-4096
	global_load_ushort v222, v241, s[0:1] offset:-2
	global_load_ushort v223, v241, s[0:1]
	global_load_ushort v224, v241, s[0:1] offset:2
	global_load_dword v225, v242, s[64:65] offset:-4096
	global_load_dword v226, v242, s[70:71] offset:-2048
	global_load_ushort v227, v241, s[0:1] offset:1022
	global_load_ushort v228, v241, s[0:1] offset:1024
	global_load_ushort v229, v241, s[0:1] offset:1026
	global_load_dword v230, v242, s[64:65] offset:-2048
	global_load_dword v231, v242, s[70:71]
	global_load_ushort v232, v241, s[0:1] offset:2046
	global_load_ushort v233, v241, s[0:1] offset:2048
	global_load_ushort v234, v241, s[0:1] offset:2050
	global_load_dword v235, v242, s[64:65]
	global_load_dword v236, v242, s[70:71] offset:2048
	global_load_ushort v237, v241, s[0:1] offset:3070
	global_load_ushort v238, v241, s[0:1] offset:3072
	global_load_ushort v239, v241, s[0:1] offset:3074
	global_load_dword v240, v242, s[64:65] offset:2048
	s_waitcnt vmcnt(20)
	v_mov_b32_e32 v10, v190
	v_add_u32_e32 v114, 0x1000, v14
	v_ashrrev_i32_e32 v115, 31, v114
	v_cmp_lt_i32_e32 vcc, s59, v14
	v_mov_b32_e32 v116, 0
	s_and_saveexec_b64 s[2:3], vcc
	s_cbranch_execz .LBB0_700
	v_mov_b32_e32 v116, v202
	s_nop 0
	v_lshlrev_b32_e32 v116, 16, v116

.LBB0_706:
	v_add_co_u32_e32 v54, vcc, 0x4000, v22
	v_add_u32_e32 v114, 0x1200, v14
	s_nop 0
	v_addc_co_u32_e32 v55, vcc, 0, v23, vcc
	v_mov_b32_e32 v10, v206
	v_ashrrev_i32_e32 v115, 31, v114
	v_cmp_lt_i32_e32 vcc, s60, v14
	v_mov_b32_e32 v15, 0
	v_mov_b32_e32 v116, 0
	s_and_saveexec_b64 s[2:3], vcc
	s_cbranch_execz .LBB0_708
	v_mov_b32_e32 v54, v207
	s_nop 0
	v_lshlrev_b32_e32 v116, 16, v54
.LBB0_708:
	s_or_b64 exec, exec, s[2:3]
	v_add_co_u32_e32 v54, vcc, 0x2000, v20
	s_movk_i32 s2, 0x2dff
	s_nop 0
	v_addc_co_u32_e32 v55, vcc, 0, v21, vcc
	v_mov_b32_e32 v117, v208
	v_cmp_gt_i32_e32 vcc, s2, v14
	s_and_saveexec_b64 s[2:3], vcc
	s_cbranch_execz .LBB0_710
	s_mov_b64 s[6:7], 0x2400
	v_mov_b32_e32 v15, v209
	s_nop 0
	v_lshlrev_b32_e32 v15, 16, v15

.LBB0_714:
	v_add_co_u32_e32 v66, vcc, 0x5000, v22
	v_mov_b32_e32 v15, 0
	s_nop 0
	v_addc_co_u32_e32 v67, vcc, 0, v23, vcc
	v_mov_b32_e32 v10, v211
	v_add_u32_e32 v66, 0x1400, v14
	v_ashrrev_i32_e32 v67, 31, v66
	v_cmp_lt_i32_e32 vcc, s61, v14
	v_mov_b32_e32 v68, 0
	s_and_saveexec_b64 s[2:3], vcc
	s_cbranch_execz .LBB0_716
	v_mov_b32_e32 v68, v212
	s_nop 0
	v_lshlrev_b32_e32 v68, 16, v68
.LBB0_716:
	s_or_b64 exec, exec, s[2:3]
	v_add_co_u32_e32 v70, vcc, 0x2000, v20
	s_movk_i32 s2, 0x2bff
	s_nop 0
	v_addc_co_u32_e32 v71, vcc, 0, v21, vcc
	v_mov_b32_e32 v69, v213
	v_cmp_gt_i32_e32 vcc, s2, v14
	s_and_saveexec_b64 s[2:3], vcc
	s_cbranch_execz .LBB0_718
	s_mov_b64 s[6:7], 0x2800
	v_mov_b32_e32 v15, v214
	s_nop 0
	v_lshlrev_b32_e32 v15, 16, v15

.LBB0_722:
	v_add_co_u32_e32 v62, vcc, 0x5000, v22
	v_add_u32_e32 v66, 0x1600, v14
	s_nop 0
	v_addc_co_u32_e32 v63, vcc, 0, v23, vcc
	v_mov_b32_e32 v10, v216
	v_ashrrev_i32_e32 v67, 31, v66
	v_cmp_lt_i32_e32 vcc, s62, v14
	v_mov_b32_e32 v15, 0
	v_mov_b32_e32 v68, 0
	s_and_saveexec_b64 s[2:3], vcc
	s_cbranch_execz .LBB0_724
	v_mov_b32_e32 v62, v217
	s_nop 0
	v_lshlrev_b32_e32 v68, 16, v62
.LBB0_724:
	s_or_b64 exec, exec, s[2:3]
	v_add_co_u32_e32 v62, vcc, 0x2000, v20
	s_movk_i32 s2, 0x29ff
	s_nop 0
	v_addc_co_u32_e32 v63, vcc, 0, v21, vcc
	v_mov_b32_e32 v69, v218
	v_cmp_gt_i32_e32 vcc, s2, v14
	s_and_saveexec_b64 s[2:3], vcc
	s_cbranch_execz .LBB0_726
	s_mov_b64 s[6:7], 0x2c00
	v_mov_b32_e32 v15, v219
	s_nop 0
	v_lshlrev_b32_e32 v15, 16, v15

.LBB0_730:
	v_add_co_u32_e32 v66, vcc, 0x6000, v22
	v_add_u32_e32 v70, 0x1800, v14
	s_nop 0
	v_addc_co_u32_e32 v67, vcc, 0, v23, vcc
	v_lshlrev_b32_e32 v241, 1, v14
	v_add_u32_e32 v241, 0x4000, v241
	v_lshlrev_b32_e32 v242, 2, v14
	v_add_u32_e32 v242, 0x9000, v242
	global_load_dword v190, v242, s[70:71] offset:-4096
	global_load_ushort v202, v241, s[0:1] offset:-2
	global_load_ushort v203, v241, s[0:1]
	global_load_ushort v204, v241, s[0:1] offset:2
	global_load_dword v205, v242, s[64:65] offset:-4096
	global_load_dword v206, v242, s[70:71] offset:-2048
	global_load_ushort v207, v241, s[0:1] offset:1022
	global_load_ushort v208, v241, s[0:1] offset:1024
	global_load_ushort v209, v241, s[0:1] offset:1026
	global_load_dword v210, v242, s[64:65] offset:-2048
	global_load_dword v211, v242, s[70:71]
	global_load_ushort v212, v241, s[0:1] offset:2046
	global_load_ushort v213, v241, s[0:1] offset:2048
	global_load_ushort v214, v241, s[0:1] offset:2050
	global_load_dword v215, v242, s[64:65]
	global_load_dword v216, v242, s[70:71] offset:2048
	global_load_ushort v217, v241, s[0:1] offset:3070
	global_load_ushort v218, v241, s[0:1] offset:3072
	global_load_ushort v219, v241, s[0:1] offset:3074
	global_load_dword v220, v242, s[64:65] offset:2048
	s_waitcnt vmcnt(20)
	v_mov_b32_e32 v10, v221
	v_ashrrev_i32_e32 v71, 31, v70
	v_cmp_lt_i32_e32 vcc, s63, v14
	v_mov_b32_e32 v15, 0
	v_mov_b32_e32 v72, 0
	s_and_saveexec_b64 s[2:3], vcc
	s_cbranch_execz .LBB0_732
	v_mov_b32_e32 v66, v222
	s_nop 0
	v_lshlrev_b32_e32 v72, 16, v66
.LBB0_732:
	s_or_b64 exec, exec, s[2:3]
	v_add_co_u32_e32 v66, vcc, 0x3000, v20
	s_movk_i32 s2, 0x27ff
	s_nop 0
	v_addc_co_u32_e32 v67, vcc, 0, v21, vcc
	v_mov_b32_e32 v73, v223
	v_cmp_gt_i32_e32 vcc, s2, v14
	s_and_saveexec_b64 s[2:3], vcc
	s_cbranch_execz .LBB0_734
	s_mov_b64 s[6:7], 0x3000
	v_mov_b32_e32 v15, v224
	s_nop 0
	v_lshlrev_b32_e32 v15, 16, v15

.LBB0_738:
	v_add_co_u32_e32 v70, vcc, 0x6000, v22
	v_add_u32_e32 v74, 0x1a00, v14
	s_nop 0
	v_addc_co_u32_e32 v71, vcc, 0, v23, vcc
	v_mov_b32_e32 v10, v226
	v_ashrrev_i32_e32 v75, 31, v74
	v_cmp_lt_i32_e32 vcc, s66, v14
	v_mov_b32_e32 v15, 0
	v_mov_b32_e32 v76, 0
	s_and_saveexec_b64 s[2:3], vcc
	s_cbranch_execz .LBB0_740
	v_mov_b32_e32 v70, v227
	s_nop 0
	v_lshlrev_b32_e32 v76, 16, v70
.LBB0_740:
	s_or_b64 exec, exec, s[2:3]
	v_add_co_u32_e32 v70, vcc, 0x3000, v20
	s_movk_i32 s2, 0x25ff
	s_nop 0
	v_addc_co_u32_e32 v71, vcc, 0, v21, vcc
	v_mov_b32_e32 v77, v228
	v_cmp_gt_i32_e32 vcc, s2, v14
	s_and_saveexec_b64 s[2:3], vcc
	s_cbranch_execz .LBB0_742
	s_mov_b64 s[6:7], 0x3400
	v_mov_b32_e32 v15, v229
	s_nop 0
	v_lshlrev_b32_e32 v15, 16, v15

.LBB0_746:
	v_add_co_u32_e32 v74, vcc, 0x7000, v22
	v_add_u32_e32 v78, 0x1c00, v14
	s_nop 0
	v_addc_co_u32_e32 v75, vcc, 0, v23, vcc
	v_mov_b32_e32 v10, v231
	v_ashrrev_i32_e32 v79, 31, v78
	v_cmp_lt_i32_e32 vcc, s67, v14
	v_mov_b32_e32 v15, 0
	v_mov_b32_e32 v80, 0
	s_and_saveexec_b64 s[2:3], vcc
	s_cbranch_execz .LBB0_748
	v_mov_b32_e32 v74, v232
	s_nop 0
	v_lshlrev_b32_e32 v80, 16, v74
.LBB0_748:
	s_or_b64 exec, exec, s[2:3]
	v_add_co_u32_e32 v74, vcc, 0x3000, v20
	s_movk_i32 s2, 0x23ff
	s_nop 0
	v_addc_co_u32_e32 v75, vcc, 0, v21, vcc
	v_mov_b32_e32 v81, v233
	v_cmp_gt_i32_e32 vcc, s2, v14
	s_and_saveexec_b64 s[2:3], vcc
	s_cbranch_execz .LBB0_750
	s_mov_b64 s[6:7], 0x3800
	v_mov_b32_e32 v15, v234
	s_nop 0
	v_lshlrev_b32_e32 v15, 16, v15

.LBB0_754:
	v_add_co_u32_e32 v78, vcc, 0x7000, v22
	v_add_u32_e32 v82, 0x1e00, v14
	s_nop 0
	v_addc_co_u32_e32 v79, vcc, 0, v23, vcc
	v_mov_b32_e32 v10, v236
	v_ashrrev_i32_e32 v83, 31, v82
	v_cmp_lt_i32_e32 vcc, s68, v14
	v_mov_b32_e32 v15, 0
	v_mov_b32_e32 v84, 0
	s_and_saveexec_b64 s[2:3], vcc
	s_cbranch_execz .LBB0_756
	v_mov_b32_e32 v78, v237
	s_nop 0
	v_lshlrev_b32_e32 v84, 16, v78
.LBB0_756:
	s_or_b64 exec, exec, s[2:3]
	v_add_co_u32_e32 v78, vcc, 0x3000, v20
	s_movk_i32 s2, 0x21ff
	s_nop 0
	v_addc_co_u32_e32 v79, vcc, 0, v21, vcc
	v_mov_b32_e32 v85, v238
	v_cmp_gt_i32_e32 vcc, s2, v14
	s_and_saveexec_b64 s[2:3], vcc
	s_cbranch_execz .LBB0_758
	s_mov_b64 s[6:7], 0x3c00
	v_mov_b32_e32 v15, v239
	s_nop 0
	v_lshlrev_b32_e32 v15, 16, v15

.LBB0_762:
	v_add_co_u32_e32 v82, vcc, 0x8000, v22
	v_mov_b32_e32 v15, 0
	s_nop 0
	v_addc_co_u32_e32 v83, vcc, 0, v23, vcc
	v_lshlrev_b32_e32 v241, 1, v14
	v_add_u32_e32 v241, 0x5000, v241
	v_lshlrev_b32_e32 v242, 2, v14
	v_add_u32_e32 v242, 0xb000, v242
	global_load_dword v221, v242, s[70:71] offset:-4096
	global_load_ushort v222, v241, s[0:1] offset:-2
	global_load_ushort v223, v241, s[0:1]
	global_load_ushort v224, v241, s[0:1] offset:2
	global_load_dword v225, v242, s[64:65] offset:-4096
	global_load_dword v226, v242, s[70:71] offset:-2048
	global_load_ushort v227, v241, s[0:1] offset:1022
	global_load_ushort v228, v241, s[0:1] offset:1024
	global_load_ushort v229, v241, s[0:1] offset:1026
	global_load_dword v230, v242, s[64:65] offset:-2048
	global_load_dword v231, v242, s[70:71]
	global_load_ushort v232, v241, s[0:1] offset:2046
	global_load_ushort v233, v241, s[0:1] offset:2048
	global_load_ushort v234, v241, s[0:1] offset:2050
	global_load_dword v235, v242, s[64:65]
	global_load_dword v236, v242, s[70:71] offset:2048
	global_load_ushort v237, v241, s[0:1] offset:3070
	global_load_ushort v238, v241, s[0:1] offset:3072
	global_load_ushort v239, v241, s[0:1] offset:3074
	global_load_dword v240, v242, s[64:65] offset:2048
	s_waitcnt vmcnt(20)
	v_mov_b32_e32 v10, v190
	v_add_u32_e32 v82, 0x2000, v14
	v_ashrrev_i32_e32 v83, 31, v82
	v_cmp_lt_i32_e32 vcc, s69, v14
	v_mov_b32_e32 v84, 0
	s_and_saveexec_b64 s[2:3], vcc
	s_cbranch_execz .LBB0_764
	v_mov_b32_e32 v84, v202
	s_nop 0
	v_lshlrev_b32_e32 v84, 16, v84

.LBB0_770:
	v_add_co_u32_e32 v4, vcc, 0x8000, v22
	v_mov_b32_e32 v7, 0
	s_nop 0
	v_addc_co_u32_e32 v5, vcc, 0, v23, vcc
	v_mov_b32_e32 v6, v206
	v_add_u32_e32 v4, 0x2200, v14
	v_ashrrev_i32_e32 v5, 31, v4
	v_cmp_lt_i32_e32 vcc, s74, v14
	v_mov_b32_e32 v10, 0
	s_and_saveexec_b64 s[2:3], vcc
	s_cbranch_execz .LBB0_772
	v_mov_b32_e32 v10, v207
	s_nop 0
	v_lshlrev_b32_e32 v10, 16, v10

.LBB0_778:
	v_add_co_u32_e32 v4, vcc, 0x9000, v22
	v_mov_b32_e32 v7, 0
	s_nop 0
	v_addc_co_u32_e32 v5, vcc, 0, v23, vcc
	v_mov_b32_e32 v6, v211
	v_add_u32_e32 v4, 0x2400, v14
	v_ashrrev_i32_e32 v5, 31, v4
	v_cmp_lt_i32_e32 vcc, s75, v14
	v_mov_b32_e32 v10, 0
	s_and_saveexec_b64 s[2:3], vcc
	s_cbranch_execz .LBB0_780
	v_mov_b32_e32 v10, v212
	s_nop 0
	v_lshlrev_b32_e32 v10, 16, v10
.LBB0_780:
	s_or_b64 exec, exec, s[2:3]
	v_add_co_u32_e32 v26, vcc, 0x4000, v20
	s_movk_i32 s2, 0x1bff
	s_nop 0
	v_addc_co_u32_e32 v27, vcc, 0, v21, vcc
	v_mov_b32_e32 v15, v213
	v_cmp_gt_i32_e32 vcc, s2, v14
	s_and_saveexec_b64 s[2:3], vcc
	s_cbranch_execz .LBB0_782
	s_mov_b64 s[6:7], 0x4800
	v_mov_b32_e32 v7, v214
	s_nop 0
	v_lshlrev_b32_e32 v7, 16, v7

.LBB0_786:
	v_add_co_u32_e32 v4, vcc, 0x9000, v22
	v_mov_b32_e32 v7, 0
	s_nop 0
	v_addc_co_u32_e32 v5, vcc, 0, v23, vcc
	v_mov_b32_e32 v6, v216
	v_add_u32_e32 v4, 0x2600, v14
	v_ashrrev_i32_e32 v5, 31, v4
	v_cmp_lt_i32_e32 vcc, s79, v14
	v_mov_b32_e32 v8, 0
	s_and_saveexec_b64 s[2:3], vcc
	s_cbranch_execz .LBB0_788
	v_mov_b32_e32 v8, v217
	s_nop 0
	v_lshlrev_b32_e32 v8, 16, v8
.LBB0_788:
	s_or_b64 exec, exec, s[2:3]
	v_add_co_u32_e32 v24, vcc, 0x4000, v20
	s_movk_i32 s2, 0x19ff
	s_nop 0
	v_addc_co_u32_e32 v25, vcc, 0, v21, vcc
	v_mov_b32_e32 v9, v218
	v_cmp_gt_i32_e32 vcc, s2, v14
	s_and_saveexec_b64 s[2:3], vcc
	s_cbranch_execz .LBB0_790
	s_mov_b64 s[6:7], 0x4c00
	v_mov_b32_e32 v7, v219
	s_nop 0
	v_lshlrev_b32_e32 v7, 16, v7

.LBB0_794:
	v_add_co_u32_e32 v4, vcc, 0xa000, v22
	v_mov_b32_e32 v7, 0
	s_nop 0
	v_addc_co_u32_e32 v5, vcc, 0, v23, vcc
	v_lshlrev_b32_e32 v241, 1, v14
	v_add_u32_e32 v241, 0x6000, v241
	v_lshlrev_b32_e32 v242, 2, v14
	v_add_u32_e32 v242, 0xd000, v242
	global_load_dword v190, v242, s[70:71] offset:-4096
	global_load_ushort v202, v241, s[0:1] offset:-2
	global_load_ushort v203, v241, s[0:1]
	global_load_ushort v204, v241, s[0:1] offset:2
	global_load_dword v205, v242, s[64:65] offset:-4096
	global_load_dword v206, v242, s[70:71] offset:-2048
	global_load_ushort v207, v241, s[0:1] offset:1022
	global_load_ushort v208, v241, s[0:1] offset:1024
	global_load_ushort v209, v241, s[0:1] offset:1026
	global_load_dword v210, v242, s[64:65] offset:-2048
	global_load_dword v211, v242, s[70:71]
	global_load_ushort v212, v241, s[0:1] offset:2046
	global_load_ushort v213, v241, s[0:1] offset:2048
	global_load_ushort v214, v241, s[0:1] offset:2050
	global_load_dword v215, v242, s[64:65]
	global_load_dword v216, v242, s[70:71] offset:2048
	global_load_ushort v217, v241, s[0:1] offset:3070
	global_load_ushort v218, v241, s[0:1] offset:3072
	global_load_ushort v219, v241, s[0:1] offset:3074
	global_load_dword v220, v242, s[64:65] offset:2048
	s_waitcnt vmcnt(20)
	v_mov_b32_e32 v6, v221
	v_add_u32_e32 v4, 0x2800, v14
	v_ashrrev_i32_e32 v5, 31, v4
	v_cmp_lt_i32_e32 vcc, s56, v14
	v_mov_b32_e32 v8, 0
	s_and_saveexec_b64 s[2:3], vcc
	s_cbranch_execz .LBB0_796
	v_mov_b32_e32 v8, v222
	s_nop 0
	v_lshlrev_b32_e32 v8, 16, v8
.LBB0_796:
	s_or_b64 exec, exec, s[2:3]
	v_add_co_u32_e32 v24, vcc, 0x5000, v20
	s_movk_i32 s2, 0x17ff
	s_nop 0
	v_addc_co_u32_e32 v25, vcc, 0, v21, vcc
	v_mov_b32_e32 v9, v223
	v_cmp_gt_i32_e32 vcc, s2, v14
	s_and_saveexec_b64 s[2:3], vcc
	s_cbranch_execz .LBB0_798
	s_mov_b64 s[6:7], 0x5000
	v_mov_b32_e32 v7, v224
	s_nop 0
	v_lshlrev_b32_e32 v7, 16, v7

.LBB0_802:
	v_add_co_u32_e32 v4, vcc, 0xa000, v22
	s_movk_i32 s2, 0xd600
	s_nop 0
	v_addc_co_u32_e32 v5, vcc, 0, v23, vcc
	v_mov_b32_e32 v6, v226
	v_add_u32_e32 v4, 0x2a00, v14
	v_ashrrev_i32_e32 v5, 31, v4
	v_cmp_lt_i32_e32 vcc, s2, v14
	v_mov_b32_e32 v7, 0
	v_mov_b32_e32 v8, 0
	s_and_saveexec_b64 s[2:3], vcc
	s_cbranch_execz .LBB0_804
	v_mov_b32_e32 v8, v227
	s_nop 0
	v_lshlrev_b32_e32 v8, 16, v8
.LBB0_804:
	s_or_b64 exec, exec, s[2:3]
	v_add_co_u32_e32 v24, vcc, 0x5000, v20
	s_movk_i32 s2, 0x15ff
	s_nop 0
	v_addc_co_u32_e32 v25, vcc, 0, v21, vcc
	v_mov_b32_e32 v9, v228
	v_cmp_gt_i32_e32 vcc, s2, v14
	s_and_saveexec_b64 s[2:3], vcc
	s_cbranch_execz .LBB0_806
	s_mov_b64 s[6:7], 0x5400
	v_mov_b32_e32 v7, v229
	s_nop 0
	v_lshlrev_b32_e32 v7, 16, v7

.LBB0_810:
	v_add_co_u32_e32 v4, vcc, 0xb000, v22
	s_movk_i32 s2, 0xd400
	s_nop 0
	v_addc_co_u32_e32 v5, vcc, 0, v23, vcc
	v_mov_b32_e32 v6, v231
	v_add_u32_e32 v4, 0x2c00, v14
	v_ashrrev_i32_e32 v5, 31, v4
	v_cmp_lt_i32_e32 vcc, s2, v14
	v_mov_b32_e32 v7, 0
	v_mov_b32_e32 v8, 0
	s_and_saveexec_b64 s[2:3], vcc
	s_cbranch_execz .LBB0_812
	v_mov_b32_e32 v8, v232
	s_nop 0
	v_lshlrev_b32_e32 v8, 16, v8
.LBB0_812:
	s_or_b64 exec, exec, s[2:3]
	v_add_co_u32_e32 v24, vcc, 0x5000, v20
	s_movk_i32 s2, 0x13ff
	s_nop 0
	v_addc_co_u32_e32 v25, vcc, 0, v21, vcc
	v_mov_b32_e32 v9, v233
	v_cmp_gt_i32_e32 vcc, s2, v14
	s_and_saveexec_b64 s[2:3], vcc
	s_cbranch_execz .LBB0_814
	s_mov_b64 s[6:7], 0x5800
	v_mov_b32_e32 v7, v234
	s_nop 0
	v_lshlrev_b32_e32 v7, 16, v7

.LBB0_818:
	v_add_co_u32_e32 v4, vcc, 0xb000, v22
	s_movk_i32 s2, 0xd200
	s_nop 0
	v_addc_co_u32_e32 v5, vcc, 0, v23, vcc
	v_mov_b32_e32 v6, v236
	v_add_u32_e32 v4, 0x2e00, v14
	v_ashrrev_i32_e32 v5, 31, v4
	v_cmp_lt_i32_e32 vcc, s2, v14
	v_mov_b32_e32 v7, 0
	v_mov_b32_e32 v8, 0
	s_and_saveexec_b64 s[2:3], vcc
	s_cbranch_execz .LBB0_820
	v_mov_b32_e32 v8, v237
	s_nop 0
	v_lshlrev_b32_e32 v8, 16, v8
.LBB0_820:
	s_or_b64 exec, exec, s[2:3]
	v_add_co_u32_e32 v24, vcc, 0x5000, v20
	s_movk_i32 s2, 0x11ff
	s_nop 0
	v_addc_co_u32_e32 v25, vcc, 0, v21, vcc
	v_mov_b32_e32 v9, v238
	v_cmp_gt_i32_e32 vcc, s2, v14
	s_and_saveexec_b64 s[2:3], vcc
	s_cbranch_execz .LBB0_822
	s_mov_b64 s[6:7], 0x5c00
	v_mov_b32_e32 v7, v239
	s_nop 0
	v_lshlrev_b32_e32 v7, 16, v7

.LBB0_826:
	v_add_co_u32_e32 v4, vcc, 0xc000, v22
	s_movk_i32 s2, 0xd000
	s_nop 0
	v_addc_co_u32_e32 v5, vcc, 0, v23, vcc
	v_lshlrev_b32_e32 v241, 1, v14
	v_add_u32_e32 v241, 0x7000, v241
	v_lshlrev_b32_e32 v242, 2, v14
	v_add_u32_e32 v242, 0xf000, v242
	global_load_dword v221, v242, s[70:71] offset:-4096
	global_load_ushort v222, v241, s[0:1] offset:-2
	global_load_ushort v223, v241, s[0:1]
	global_load_ushort v224, v241, s[0:1] offset:2
	global_load_dword v225, v242, s[64:65] offset:-4096
	global_load_dword v226, v242, s[70:71] offset:-2048
	global_load_ushort v227, v241, s[0:1] offset:1022
	global_load_ushort v228, v241, s[0:1] offset:1024
	global_load_ushort v229, v241, s[0:1] offset:1026
	global_load_dword v230, v242, s[64:65] offset:-2048
	global_load_dword v231, v242, s[70:71]
	global_load_ushort v232, v241, s[0:1] offset:2046
	global_load_ushort v233, v241, s[0:1] offset:2048
	global_load_ushort v234, v241, s[0:1] offset:2050
	global_load_dword v235, v242, s[64:65]
	global_load_dword v236, v242, s[70:71] offset:2048
	global_load_ushort v237, v241, s[0:1] offset:3070
	global_load_ushort v238, v241, s[0:1] offset:3072
	global_load_ushort v239, v241, s[0:1] offset:3074
	global_load_dword v240, v242, s[64:65] offset:2048
	s_waitcnt vmcnt(20)
	v_mov_b32_e32 v6, v190
	v_add_u32_e32 v4, 0x3000, v14
	v_ashrrev_i32_e32 v5, 31, v4
	v_cmp_lt_i32_e32 vcc, s2, v14
	v_mov_b32_e32 v7, 0
	v_mov_b32_e32 v8, 0
	s_and_saveexec_b64 s[2:3], vcc
	s_cbranch_execz .LBB0_828
	v_mov_b32_e32 v8, v202
	s_nop 0
	v_lshlrev_b32_e32 v8, 16, v8
.LBB0_828:
	s_or_b64 exec, exec, s[2:3]
	v_add_co_u32_e32 v24, vcc, 0x6000, v20
	s_movk_i32 s2, 0xfff
	s_nop 0
	v_addc_co_u32_e32 v25, vcc, 0, v21, vcc
	v_mov_b32_e32 v9, v203
	v_cmp_gt_i32_e32 vcc, s2, v14
	s_and_saveexec_b64 s[2:3], vcc
	s_cbranch_execz .LBB0_830
	s_mov_b64 s[6:7], 0x6000
	v_mov_b32_e32 v7, v204
	s_nop 0
	v_lshlrev_b32_e32 v7, 16, v7

.LBB0_834:
	v_add_co_u32_e32 v4, vcc, 0xc000, v22
	v_mov_b32_e32 v7, 0
	s_nop 0
	v_addc_co_u32_e32 v5, vcc, 0, v23, vcc
	v_mov_b32_e32 v6, v206
	v_add_u32_e32 v4, 0x3200, v14
	v_ashrrev_i32_e32 v5, 31, v4
	v_cmp_lt_i32_e32 vcc, s84, v14
	v_mov_b32_e32 v8, 0
	s_and_saveexec_b64 s[2:3], vcc
	s_cbranch_execz .LBB0_836
	v_mov_b32_e32 v8, v207
	s_nop 0
	v_lshlrev_b32_e32 v8, 16, v8
.LBB0_836:
	s_or_b64 exec, exec, s[2:3]
	v_add_co_u32_e32 v24, vcc, 0x6000, v20
	s_movk_i32 s2, 0xdff
	s_nop 0
	v_addc_co_u32_e32 v25, vcc, 0, v21, vcc
	v_mov_b32_e32 v9, v208
	v_cmp_gt_i32_e32 vcc, s2, v14
	s_and_saveexec_b64 s[2:3], vcc
	s_cbranch_execz .LBB0_838
	s_mov_b64 s[6:7], 0x6400
	v_mov_b32_e32 v7, v209
	s_nop 0
	v_lshlrev_b32_e32 v7, 16, v7

.LBB0_842:
	v_add_co_u32_e32 v4, vcc, 0xd000, v22
	s_movk_i32 s2, 0xcc00
	s_nop 0
	v_addc_co_u32_e32 v5, vcc, 0, v23, vcc
	v_mov_b32_e32 v6, v211
	v_add_u32_e32 v4, 0x3400, v14
	v_ashrrev_i32_e32 v5, 31, v4
	v_cmp_lt_i32_e32 vcc, s2, v14
	v_mov_b32_e32 v7, 0
	v_mov_b32_e32 v8, 0
	s_and_saveexec_b64 s[2:3], vcc
	s_cbranch_execz .LBB0_844
	v_mov_b32_e32 v8, v212
	s_nop 0
	v_lshlrev_b32_e32 v8, 16, v8
.LBB0_844:
	s_or_b64 exec, exec, s[2:3]
	v_add_co_u32_e32 v24, vcc, 0x6000, v20
	s_movk_i32 s2, 0xbff
	s_nop 0
	v_addc_co_u32_e32 v25, vcc, 0, v21, vcc
	v_mov_b32_e32 v9, v213
	v_cmp_gt_i32_e32 vcc, s2, v14
	s_and_saveexec_b64 s[2:3], vcc
	s_cbranch_execz .LBB0_846
	s_mov_b64 s[6:7], 0x6800
	v_mov_b32_e32 v7, v214
	s_nop 0
	v_lshlrev_b32_e32 v7, 16, v7

.LBB0_850:
	v_add_co_u32_e32 v4, vcc, 0xd000, v22
	s_movk_i32 s2, 0xca00
	s_nop 0
	v_addc_co_u32_e32 v5, vcc, 0, v23, vcc
	v_mov_b32_e32 v6, v216
	v_add_u32_e32 v4, 0x3600, v14
	v_ashrrev_i32_e32 v5, 31, v4
	v_cmp_lt_i32_e32 vcc, s2, v14
	v_mov_b32_e32 v7, 0
	v_mov_b32_e32 v8, 0
	s_and_saveexec_b64 s[2:3], vcc
	s_cbranch_execz .LBB0_852
	v_mov_b32_e32 v8, v217
	s_nop 0
	v_lshlrev_b32_e32 v8, 16, v8
.LBB0_852:
	s_or_b64 exec, exec, s[2:3]
	v_add_co_u32_e32 v24, vcc, 0x6000, v20
	s_movk_i32 s2, 0x9ff
	s_nop 0
	v_addc_co_u32_e32 v25, vcc, 0, v21, vcc
	v_mov_b32_e32 v9, v218
	v_cmp_gt_i32_e32 vcc, s2, v14
	s_and_saveexec_b64 s[2:3], vcc
	s_cbranch_execz .LBB0_854
	s_mov_b64 s[6:7], 0x6c00
	v_mov_b32_e32 v7, v219
	s_nop 0
	v_lshlrev_b32_e32 v7, 16, v7

.LBB0_858:
	v_add_co_u32_e32 v4, vcc, 0xe000, v22
	s_movk_i32 s2, 0xc800
	s_nop 0
	v_addc_co_u32_e32 v5, vcc, 0, v23, vcc
	s_waitcnt vmcnt(0)
	v_mov_b32_e32 v6, v221
	v_add_u32_e32 v4, 0x3800, v14
	v_ashrrev_i32_e32 v5, 31, v4
	v_cmp_lt_i32_e32 vcc, s2, v14
	v_mov_b32_e32 v7, 0
	v_mov_b32_e32 v8, 0
	s_and_saveexec_b64 s[2:3], vcc
	s_cbranch_execz .LBB0_860
	v_mov_b32_e32 v8, v222
	s_nop 0
	v_lshlrev_b32_e32 v8, 16, v8
.LBB0_860:
	s_or_b64 exec, exec, s[2:3]
	v_add_co_u32_e32 v24, vcc, 0x7000, v20
	s_movk_i32 s2, 0x7ff
	s_nop 0
	v_addc_co_u32_e32 v25, vcc, 0, v21, vcc
	v_mov_b32_e32 v9, v223
	v_cmp_gt_i32_e32 vcc, s2, v14
	s_and_saveexec_b64 s[2:3], vcc
	s_cbranch_execz .LBB0_862
	s_mov_b64 s[6:7], 0x7000
	v_mov_b32_e32 v7, v224
	s_nop 0
	v_lshlrev_b32_e32 v7, 16, v7

.LBB0_866:
	v_add_co_u32_e32 v4, vcc, 0xe000, v22
	s_movk_i32 s2, 0xc600
	s_nop 0
	v_addc_co_u32_e32 v5, vcc, 0, v23, vcc
	v_mov_b32_e32 v6, v226
	v_add_u32_e32 v4, 0x3a00, v14
	v_ashrrev_i32_e32 v5, 31, v4
	v_cmp_lt_i32_e32 vcc, s2, v14
	v_mov_b32_e32 v7, 0
	v_mov_b32_e32 v8, 0
	s_and_saveexec_b64 s[2:3], vcc
	s_cbranch_execz .LBB0_868
	v_mov_b32_e32 v8, v227
	s_nop 0
	v_lshlrev_b32_e32 v8, 16, v8
.LBB0_868:
	s_or_b64 exec, exec, s[2:3]
	v_add_co_u32_e32 v24, vcc, 0x7000, v20
	s_movk_i32 s2, 0x5ff
	s_nop 0
	v_addc_co_u32_e32 v25, vcc, 0, v21, vcc
	v_mov_b32_e32 v9, v228
	v_cmp_gt_i32_e32 vcc, s2, v14
	s_and_saveexec_b64 s[2:3], vcc
	s_cbranch_execz .LBB0_870
	s_mov_b64 s[6:7], 0x7400
	v_mov_b32_e32 v7, v229
	s_nop 0
	v_lshlrev_b32_e32 v7, 16, v7

.LBB0_874:
	v_add_co_u32_e32 v4, vcc, 0xf000, v22
	s_movk_i32 s2, 0xc400
	s_nop 0
	v_addc_co_u32_e32 v5, vcc, 0, v23, vcc
	v_mov_b32_e32 v6, v231
	v_add_u32_e32 v4, 0x3c00, v14
	v_ashrrev_i32_e32 v5, 31, v4
	v_cmp_lt_i32_e32 vcc, s2, v14
	v_mov_b32_e32 v7, 0
	v_mov_b32_e32 v8, 0
	s_and_saveexec_b64 s[2:3], vcc
	s_cbranch_execz .LBB0_876
	v_mov_b32_e32 v8, v232
	s_nop 0
	v_lshlrev_b32_e32 v8, 16, v8
.LBB0_876:
	s_or_b64 exec, exec, s[2:3]
	v_add_co_u32_e32 v24, vcc, 0x7000, v20
	s_movk_i32 s2, 0x3ff
	s_nop 0
	v_addc_co_u32_e32 v25, vcc, 0, v21, vcc
	v_mov_b32_e32 v9, v233
	v_cmp_gt_i32_e32 vcc, s2, v14
	s_and_saveexec_b64 s[2:3], vcc
	s_cbranch_execz .LBB0_878
	s_mov_b64 s[6:7], 0x7800
	v_mov_b32_e32 v7, v234
	s_nop 0
	v_lshlrev_b32_e32 v7, 16, v7

.LBB0_882:
	v_add_co_u32_e32 v4, vcc, 0xf000, v22
	s_movk_i32 s2, 0xc200
	s_nop 0
	v_addc_co_u32_e32 v5, vcc, 0, v23, vcc
	v_mov_b32_e32 v6, v236
	v_add_u32_e32 v4, 0x3e00, v14
	v_ashrrev_i32_e32 v5, 31, v4
	v_cmp_lt_i32_e32 vcc, s2, v14
	v_mov_b32_e32 v7, 0
	v_mov_b32_e32 v8, 0
	s_and_saveexec_b64 s[2:3], vcc
	s_cbranch_execz .LBB0_884
	v_mov_b32_e32 v8, v237
	s_nop 0
	v_lshlrev_b32_e32 v8, 16, v8
.LBB0_884:
	s_or_b64 exec, exec, s[2:3]
	v_add_co_u32_e32 v22, vcc, 0x7000, v20
	s_movk_i32 s0, 0x1ff
	s_nop 0
	v_addc_co_u32_e32 v23, vcc, 0, v21, vcc
	v_mov_b32_e32 v9, v238
	v_cmp_gt_i32_e32 vcc, s0, v14
	s_and_saveexec_b64 s[0:1], vcc
	s_cbranch_execz .LBB0_886
	s_mov_b64 s[2:3], 0x7c00
	v_mov_b32_e32 v7, v239
	s_nop 0
	v_lshlrev_b32_e32 v7, 16, v7

.LBB0_2730:
	s_or_b64 exec, exec, s[0:1]
	s_add_i32 s0, 0, 0x21000
	v_mov_b32_e32 v2, s0
	v_readlane_b32 s0, v251, 26
	v_mov_b32_e32 v92, v174
	s_waitcnt lgkmcnt(0)
	v_mov_b32_e32 v3, s0
	s_barrier
	ds_read_b128 v[6:9], v2
	ds_read_b128 v[2:5], v3
	v_mov_b32_e32 v60, v165
	v_mov_b32_e32 v34, v166
	v_mov_b32_e32 v62, v167
	v_mov_b32_e32 v32, v168
	v_mov_b32_e32 v64, v169
	v_mov_b32_e32 v38, v170
	v_mov_b32_e32 v66, v171
	v_pk_add_f32 v[68:69], v[14:15], v[42:43]
	v_pk_add_f32 v[14:15], v[14:15], v[42:43] neg_lo:[0,1] neg_hi:[0,1]
	s_nop 0
	v_mov_b32_e32 v13, v15
	v_mov_b32_e32 v10, v14
	v_mov_b32_e32 v42, v15
	v_mov_b32_e32 v43, v11
	v_pk_mul_f32 v[14:15], v[12:13], v[66:67] op_sel_hi:[1,0] neg_lo:[0,1] neg_hi:[0,1]
	v_pk_add_f32 v[70:71], v[18:19], v[52:53]
	v_pk_fma_f32 v[42:43], v[42:43], v[60:61], v[14:15] op_sel_hi:[1,0,1]
	v_pk_add_f32 v[14:15], v[16:17], v[48:49]
	v_pk_add_f32 v[48:49], v[16:17], v[48:49] neg_lo:[0,1] neg_hi:[0,1]
	v_mov_b32_e32 v17, v11
	v_mov_b32_e32 v13, v48
	v_mov_b32_e32 v16, v48
	v_pk_mul_f32 v[54:55], v[12:13], v[38:39] op_sel_hi:[1,0] neg_lo:[0,1] neg_hi:[0,1]
	v_mov_b32_e32 v13, v49
	v_pk_add_f32 v[18:19], v[18:19], v[52:53] neg_lo:[0,1] neg_hi:[0,1]
	v_pk_fma_f32 v[16:17], v[16:17], v[34:35], v[54:55] op_sel_hi:[1,0,1]
	v_mov_b32_e32 v54, v49
	v_mov_b32_e32 v55, v11
	v_pk_mul_f32 v[48:49], v[12:13], v[64:65] op_sel_hi:[1,0] neg_lo:[0,1] neg_hi:[0,1]
	v_mov_b32_e32 v13, v18
	v_pk_fma_f32 v[48:49], v[54:55], v[62:63], v[48:49] op_sel_hi:[1,0,1]
	v_mov_b32_e32 v52, v18
	v_mov_b32_e32 v53, v11
	v_pk_mul_f32 v[54:55], v[12:13], v[32:33] op_sel_hi:[1,0] neg_lo:[0,1] neg_hi:[0,1]
	v_mov_b32_e32 v13, v19
	v_pk_fma_f32 v[52:53], v[52:53], v[32:33], v[54:55] op_sel_hi:[1,0,1]
	v_mov_b32_e32 v54, v19
	v_mov_b32_e32 v55, v11
	v_pk_add_f32 v[18:19], v[20:21], v[50:51]
	v_pk_add_f32 v[20:21], v[20:21], v[50:51] neg_lo:[0,1] neg_hi:[0,1]
	v_pk_mul_f32 v[54:55], v[54:55], v[64:65] op_sel_hi:[1,0]
	v_mov_b32_e32 v50, v20
	v_mov_b32_e32 v51, v11
	v_pk_fma_f32 v[54:55], v[12:13], v[62:63], v[54:55] op_sel_hi:[1,0,1] neg_lo:[0,1,0] neg_hi:[0,1,0]
	v_pk_mul_f32 v[50:51], v[50:51], v[38:39] op_sel_hi:[1,0]
	v_mov_b32_e32 v13, v20
	v_pk_fma_f32 v[58:59], v[12:13], v[34:35], v[50:51] op_sel_hi:[1,0,1] neg_lo:[0,1,0] neg_hi:[0,1,0]
	v_mov_b32_e32 v50, v21
	v_mov_b32_e32 v51, v11
	v_pk_mul_f32 v[50:51], v[50:51], v[66:67] op_sel_hi:[1,0]
	v_mov_b32_e32 v13, v21
	v_pk_add_f32 v[20:21], v[24:25], v[46:47]
	v_pk_add_f32 v[24:25], v[24:25], v[46:47] neg_lo:[0,1] neg_hi:[0,1]
	v_pk_fma_f32 v[56:57], v[12:13], v[60:61], v[50:51] op_sel_hi:[1,0,1] neg_lo:[0,1,0] neg_hi:[0,1,0]
	v_xor_b32_e32 v73, 0x80000000, v24
	v_mov_b32_e32 v46, v25
	v_mov_b32_e32 v47, v11
	v_mov_b32_e32 v13, v25
	v_pk_add_f32 v[24:25], v[28:29], v[44:45]
	v_pk_add_f32 v[28:29], v[28:29], v[44:45] neg_lo:[0,1] neg_hi:[0,1]
	v_pk_mul_f32 v[46:47], v[46:47], v[66:67] op_sel_hi:[1,0] neg_lo:[0,1] neg_hi:[0,1]
	v_mov_b32_e32 v44, v28
	v_mov_b32_e32 v45, v11
	v_pk_fma_f32 v[74:75], v[12:13], v[60:61], v[46:47] op_sel_hi:[1,0,1] neg_lo:[0,1,0] neg_hi:[0,1,0]
	v_pk_mul_f32 v[44:45], v[44:45], v[38:39] op_sel_hi:[1,0] neg_lo:[0,1] neg_hi:[0,1]
	v_mov_b32_e32 v13, v28
	v_pk_fma_f32 v[76:77], v[12:13], v[34:35], v[44:45] op_sel_hi:[1,0,1] neg_lo:[0,1,0] neg_hi:[0,1,0]
	v_mov_b32_e32 v44, v29
	v_mov_b32_e32 v45, v11
	v_pk_mul_f32 v[44:45], v[44:45], v[64:65] op_sel_hi:[1,0] neg_lo:[0,1] neg_hi:[0,1]
	v_mov_b32_e32 v13, v29
	v_pk_add_f32 v[28:29], v[30:31], v[40:41]
	v_pk_add_f32 v[30:31], v[30:31], v[40:41] neg_lo:[0,1] neg_hi:[0,1]
	v_pk_fma_f32 v[78:79], v[12:13], v[62:63], v[44:45] op_sel_hi:[1,0,1] neg_lo:[0,1,0] neg_hi:[0,1,0]
	v_mov_b32_e32 v13, v30
	v_mov_b32_e32 v40, v30
	v_mov_b32_e32 v41, v11
	v_pk_mul_f32 v[44:45], v[12:13], v[32:33] op_sel_hi:[1,0] neg_lo:[0,1] neg_hi:[0,1]
	v_mov_b32_e32 v13, v31
	v_pk_fma_f32 v[80:81], v[40:41], v[32:33], v[44:45] op_sel_hi:[1,0,1] neg_lo:[0,1,0] neg_hi:[0,1,0]
	v_mov_b32_e32 v40, v31
	v_pk_mul_f32 v[30:31], v[12:13], v[64:65] op_sel_hi:[1,0] neg_lo:[0,1] neg_hi:[0,1]
	v_mov_b32_e32 v84, v11
	v_pk_fma_f32 v[62:63], v[40:41], v[62:63], v[30:31] op_sel_hi:[1,0,1] neg_lo:[0,1,0] neg_hi:[0,1,0]
	v_pk_add_f32 v[30:31], v[26:27], v[36:37]
	v_pk_add_f32 v[26:27], v[26:27], v[36:37] neg_lo:[0,1] neg_hi:[0,1]
	v_mov_b32_e32 v37, v11
	v_mov_b32_e32 v13, v26
	v_mov_b32_e32 v36, v26
	v_pk_mul_f32 v[40:41], v[12:13], v[38:39] op_sel_hi:[1,0] neg_lo:[0,1] neg_hi:[0,1]
	v_mov_b32_e32 v13, v27
	v_pk_fma_f32 v[64:65], v[36:37], v[34:35], v[40:41] op_sel_hi:[1,0,1] neg_lo:[0,1,0] neg_hi:[0,1,0]
	v_mov_b32_e32 v36, v27
	v_pk_mul_f32 v[26:27], v[12:13], v[66:67] op_sel_hi:[1,0] neg_lo:[0,1] neg_hi:[0,1]
	v_mov_b32_e32 v41, v11
	v_pk_fma_f32 v[66:67], v[36:37], v[60:61], v[26:27] op_sel_hi:[1,0,1] neg_lo:[0,1,0] neg_hi:[0,1,0]
	v_pk_add_f32 v[26:27], v[68:69], v[20:21] neg_lo:[0,1] neg_hi:[0,1]
	v_pk_add_f32 v[20:21], v[68:69], v[20:21]
	v_mov_b32_e32 v13, v27
	v_mov_b32_e32 v36, v26
	v_mov_b32_e32 v40, v27
	v_pk_mul_f32 v[26:27], v[12:13], v[38:39] op_sel_hi:[1,0] neg_lo:[0,1] neg_hi:[0,1]
	v_mov_b32_e32 v61, v11
	v_pk_fma_f32 v[44:45], v[40:41], v[34:35], v[26:27] op_sel_hi:[1,0,1]
	v_pk_add_f32 v[26:27], v[14:15], v[24:25] neg_lo:[0,1] neg_hi:[0,1]
	v_pk_add_f32 v[14:15], v[14:15], v[24:25]
	v_mov_b32_e32 v13, v26
	v_mov_b32_e32 v40, v26
	v_pk_mul_f32 v[46:47], v[12:13], v[32:33] op_sel_hi:[1,0] neg_lo:[0,1] neg_hi:[0,1]
	v_mov_b32_e32 v13, v27
	v_pk_fma_f32 v[50:51], v[40:41], v[32:33], v[46:47] op_sel_hi:[1,0,1]
	v_mov_b32_e32 v40, v27
	v_pk_mul_f32 v[40:41], v[40:41], v[38:39] op_sel_hi:[1,0]
	v_pk_add_f32 v[26:27], v[70:71], v[28:29] neg_lo:[0,1] neg_hi:[0,1]
	v_pk_fma_f32 v[82:83], v[12:13], v[34:35], v[40:41] op_sel_hi:[1,0,1] neg_lo:[0,1,0] neg_hi:[0,1,0]
	v_mov_b32_e32 v40, v27
	v_mov_b32_e32 v41, v11
	v_xor_b32_e32 v85, 0x80000000, v26
	v_pk_mul_f32 v[40:41], v[40:41], v[38:39] op_sel_hi:[1,0] neg_lo:[0,1] neg_hi:[0,1]
	v_mov_b32_e32 v13, v27
	v_pk_add_f32 v[26:27], v[18:19], v[30:31] neg_lo:[0,1] neg_hi:[0,1]
	v_pk_fma_f32 v[86:87], v[12:13], v[34:35], v[40:41] op_sel_hi:[1,0,1] neg_lo:[0,1,0] neg_hi:[0,1,0]
	v_mov_b32_e32 v13, v26
	v_mov_b32_e32 v40, v26
	v_mov_b32_e32 v41, v11
	v_pk_mul_f32 v[46:47], v[12:13], v[32:33] op_sel_hi:[1,0] neg_lo:[0,1] neg_hi:[0,1]
	v_mov_b32_e32 v13, v27
	v_pk_fma_f32 v[88:89], v[40:41], v[32:33], v[46:47] op_sel_hi:[1,0,1] neg_lo:[0,1,0] neg_hi:[0,1,0]
	v_mov_b32_e32 v40, v27
	v_pk_mul_f32 v[26:27], v[12:13], v[38:39] op_sel_hi:[1,0] neg_lo:[0,1] neg_hi:[0,1]
	v_pk_add_f32 v[24:25], v[70:71], v[28:29]
	v_pk_fma_f32 v[90:91], v[40:41], v[34:35], v[26:27] op_sel_hi:[1,0,1] neg_lo:[0,1,0] neg_hi:[0,1,0]
	v_pk_add_f32 v[26:27], v[20:21], v[24:25] neg_lo:[0,1] neg_hi:[0,1]
	v_pk_add_f32 v[18:19], v[18:19], v[30:31]
	v_mov_b32_e32 v13, v27
	v_mov_b32_e32 v28, v26
	v_pk_add_f32 v[20:21], v[20:21], v[24:25]
	v_mov_b32_e32 v24, v27
	v_mov_b32_e32 v25, v11
	v_pk_mul_f32 v[26:27], v[12:13], v[32:33] op_sel_hi:[1,0] neg_lo:[0,1] neg_hi:[0,1]
	v_mov_b32_e32 v29, v11
	v_pk_fma_f32 v[24:25], v[24:25], v[32:33], v[26:27] op_sel_hi:[1,0,1]
	v_pk_add_f32 v[26:27], v[14:15], v[18:19] neg_lo:[0,1] neg_hi:[0,1]
	v_pk_add_f32 v[14:15], v[14:15], v[18:19]
	v_mov_b32_e32 v13, v27
	v_xor_b32_e32 v41, 0x80000000, v26
	v_mov_b32_e32 v18, v27
	v_mov_b32_e32 v19, v11
	v_pk_mul_f32 v[26:27], v[12:13], v[32:33] op_sel_hi:[1,0] neg_lo:[0,1] neg_hi:[0,1]
	v_pk_add_f32 v[30:31], v[20:21], v[14:15]
	v_pk_fma_f32 v[18:19], v[18:19], v[32:33], v[26:27] op_sel_hi:[1,0,1] neg_lo:[0,1,0] neg_hi:[0,1,0]
	v_pk_add_f32 v[26:27], v[20:21], v[14:15] neg_lo:[0,1] neg_hi:[0,1]
	v_mov_b32_e32 v40, v11
	v_pk_add_f32 v[14:15], v[26:27], 0 neg_lo:[1,1] neg_hi:[1,1]
	v_mov_b32_e32 v60, v26
	v_mov_b32_e32 v14, v11
	v_pk_add_f32 v[26:27], v[24:25], v[18:19]
	v_pk_add_f32 v[18:19], v[24:25], v[18:19] neg_lo:[0,1] neg_hi:[0,1]
	v_pk_add_f32 v[46:47], v[60:61], v[14:15]
	v_pk_add_f32 v[20:21], v[60:61], v[14:15] neg_lo:[0,1] neg_hi:[0,1]
	v_pk_add_f32 v[14:15], v[28:29], v[40:41]
	v_pk_add_f32 v[28:29], v[28:29], v[40:41] neg_lo:[0,1] neg_hi:[0,1]
	v_pk_add_f32 v[60:61], v[14:15], v[26:27]
	v_pk_add_f32 v[26:27], v[14:15], v[26:27] neg_lo:[0,1] neg_hi:[0,1]
	v_pk_add_f32 v[40:41], v[28:29], v[18:19] op_sel:[0,1] op_sel_hi:[1,0] neg_hi:[0,1]
	v_pk_add_f32 v[14:15], v[28:29], v[18:19] op_sel:[0,1] op_sel_hi:[1,0] neg_lo:[0,1]
	v_pk_add_f32 v[18:19], v[36:37], v[84:85]
	v_pk_add_f32 v[28:29], v[36:37], v[84:85] neg_lo:[0,1] neg_hi:[0,1]
	v_pk_add_f32 v[36:37], v[44:45], v[86:87] neg_lo:[0,1] neg_hi:[0,1]
	v_pk_add_f32 v[24:25], v[44:45], v[86:87]
	v_pk_mul_f32 v[44:45], v[32:33], v[36:37] op_sel:[0,1] op_sel_hi:[0,0] neg_lo:[1,1] neg_hi:[1,0]
	v_pk_fma_f32 v[44:45], v[32:33], v[36:37], v[44:45] op_sel_hi:[0,1,1]
	v_pk_add_f32 v[36:37], v[50:51], v[88:89]
	v_pk_add_f32 v[50:51], v[50:51], v[88:89] neg_lo:[0,1] neg_hi:[0,1]
	v_pk_add_f32 v[70:71], v[82:83], v[90:91] neg_lo:[0,1] neg_hi:[0,1]
	v_xor_b32_e32 v69, 0x80000000, v50
	v_mov_b32_e32 v68, v51
	v_pk_add_f32 v[50:51], v[82:83], v[90:91]
	v_pk_mul_f32 v[82:83], v[32:33], v[70:71] op_sel:[0,1] op_sel_hi:[0,0] neg_lo:[1,1] neg_hi:[1,0]
	v_pk_fma_f32 v[70:71], v[32:33], v[70:71], v[82:83] op_sel_hi:[0,1,1] neg_lo:[1,0,0] neg_hi:[1,0,0]
	v_pk_add_f32 v[82:83], v[18:19], v[36:37]
	v_pk_add_f32 v[18:19], v[18:19], v[36:37] neg_lo:[0,1] neg_hi:[0,1]
	v_pk_add_f32 v[36:37], v[24:25], v[50:51]
	v_pk_add_f32 v[24:25], v[24:25], v[50:51] neg_lo:[0,1] neg_hi:[0,1]
	v_mov_b32_e32 v72, v11
	v_pk_add_f32 v[50:51], v[18:19], v[24:25] op_sel:[0,1] op_sel_hi:[1,0] neg_hi:[0,1]
	v_pk_add_f32 v[24:25], v[18:19], v[24:25] op_sel:[0,1] op_sel_hi:[1,0] neg_lo:[0,1]
	v_pk_add_f32 v[18:19], v[28:29], v[68:69]
	v_pk_add_f32 v[68:69], v[28:29], v[68:69] neg_lo:[0,1] neg_hi:[0,1]
	v_pk_add_f32 v[28:29], v[44:45], v[70:71]
	v_pk_add_f32 v[44:45], v[44:45], v[70:71] neg_lo:[0,1] neg_hi:[0,1]
	v_pk_add_f32 v[86:87], v[82:83], v[36:37]
	v_xor_b32_e32 v71, 0x80000000, v44
	v_mov_b32_e32 v70, v45
	v_pk_add_f32 v[36:37], v[82:83], v[36:37] neg_lo:[0,1] neg_hi:[0,1]
	v_pk_add_f32 v[82:83], v[18:19], v[28:29]
	v_pk_add_f32 v[28:29], v[18:19], v[28:29] neg_lo:[0,1] neg_hi:[0,1]
	v_pk_add_f32 v[44:45], v[68:69], v[70:71]
	v_pk_add_f32 v[18:19], v[68:69], v[70:71] neg_lo:[0,1] neg_hi:[0,1]
	v_pk_add_f32 v[68:69], v[10:11], v[72:73]
	v_pk_add_f32 v[70:71], v[10:11], v[72:73] neg_lo:[0,1] neg_hi:[0,1]
	v_pk_add_f32 v[72:73], v[42:43], v[74:75]
	v_pk_add_f32 v[42:43], v[42:43], v[74:75] neg_lo:[0,1] neg_hi:[0,1]
	v_add_f32_e32 v10, v30, v31
	v_pk_mul_f32 v[74:75], v[38:39], v[42:43] op_sel:[0,1] op_sel_hi:[0,0] neg_lo:[1,1] neg_hi:[1,0]
	v_pk_fma_f32 v[42:43], v[34:35], v[42:43], v[74:75] op_sel_hi:[0,1,1]
	v_pk_add_f32 v[74:75], v[16:17], v[76:77]
	v_pk_add_f32 v[16:17], v[16:17], v[76:77] neg_lo:[0,1] neg_hi:[0,1]
	v_lshl_add_u32 v13, v92, 3, 0
	v_pk_mul_f32 v[76:77], v[32:33], v[16:17] op_sel:[0,1] op_sel_hi:[0,0] neg_lo:[1,1] neg_hi:[1,0]
	v_pk_fma_f32 v[16:17], v[32:33], v[16:17], v[76:77] op_sel_hi:[0,1,1]
	v_pk_add_f32 v[76:77], v[48:49], v[78:79]
	v_pk_add_f32 v[48:49], v[48:49], v[78:79] neg_lo:[0,1] neg_hi:[0,1]
	s_nop 0
	v_pk_mul_f32 v[78:79], v[34:35], v[48:49] op_sel:[0,1] op_sel_hi:[0,0] neg_lo:[1,1] neg_hi:[1,0]
	v_pk_fma_f32 v[78:79], v[38:39], v[48:49], v[78:79] op_sel_hi:[0,1,1]
	v_pk_add_f32 v[48:49], v[52:53], v[80:81]
	v_pk_add_f32 v[52:53], v[52:53], v[80:81] neg_lo:[0,1] neg_hi:[0,1]
	s_nop 0
	v_xor_b32_e32 v81, 0x80000000, v52
	v_mov_b32_e32 v80, v53
	v_pk_add_f32 v[52:53], v[54:55], v[62:63]
	v_pk_add_f32 v[54:55], v[54:55], v[62:63] neg_lo:[0,1] neg_hi:[0,1]
	s_nop 0
	v_pk_mul_f32 v[62:63], v[34:35], v[54:55] op_sel:[0,1] op_sel_hi:[0,0] neg_lo:[1,1] neg_hi:[1,0]
	v_pk_fma_f32 v[62:63], v[38:39], v[54:55], v[62:63] op_sel_hi:[0,1,1] neg_lo:[1,0,0] neg_hi:[1,0,0]
	v_pk_add_f32 v[54:55], v[58:59], v[64:65]
	v_pk_add_f32 v[58:59], v[58:59], v[64:65] neg_lo:[0,1] neg_hi:[0,1]
	s_nop 0
	v_pk_mul_f32 v[64:65], v[32:33], v[58:59] op_sel:[0,1] op_sel_hi:[0,0] neg_lo:[1,1] neg_hi:[1,0]
	v_pk_fma_f32 v[58:59], v[32:33], v[58:59], v[64:65] op_sel_hi:[0,1,1] neg_lo:[1,0,0] neg_hi:[1,0,0]
	v_pk_add_f32 v[64:65], v[56:57], v[66:67]
	v_pk_add_f32 v[56:57], v[56:57], v[66:67] neg_lo:[0,1] neg_hi:[0,1]
	s_nop 0
	v_pk_mul_f32 v[38:39], v[38:39], v[56:57] op_sel:[0,1] op_sel_hi:[0,0] neg_lo:[1,1] neg_hi:[1,0]
	v_pk_fma_f32 v[56:57], v[34:35], v[56:57], v[38:39] op_sel_hi:[0,1,1] neg_lo:[1,0,0] neg_hi:[1,0,0]
	v_pk_add_f32 v[38:39], v[52:53], v[72:73]
	v_pk_add_f32 v[52:53], v[72:73], v[52:53] neg_lo:[0,1] neg_hi:[0,1]
	v_pk_add_f32 v[34:35], v[68:69], v[48:49]
	v_pk_mul_f32 v[66:67], v[32:33], v[52:53] op_sel:[0,1] op_sel_hi:[0,0] neg_lo:[1,1] neg_hi:[1,0]
	v_pk_fma_f32 v[52:53], v[32:33], v[52:53], v[66:67] op_sel_hi:[0,1,1]
	v_pk_add_f32 v[66:67], v[74:75], v[54:55]
	v_pk_add_f32 v[54:55], v[74:75], v[54:55] neg_lo:[0,1] neg_hi:[0,1]
	v_pk_add_f32 v[48:49], v[68:69], v[48:49] neg_lo:[0,1] neg_hi:[0,1]
	v_xor_b32_e32 v69, 0x80000000, v54
	v_mov_b32_e32 v68, v55
	v_pk_add_f32 v[54:55], v[76:77], v[64:65]
	v_pk_add_f32 v[64:65], v[76:77], v[64:65] neg_lo:[0,1] neg_hi:[0,1]
	s_nop 0
	v_pk_mul_f32 v[72:73], v[32:33], v[64:65] op_sel:[0,1] op_sel_hi:[0,0] neg_lo:[1,1] neg_hi:[1,0]
	v_pk_fma_f32 v[64:65], v[32:33], v[64:65], v[72:73] op_sel_hi:[0,1,1] neg_lo:[1,0,0] neg_hi:[1,0,0]
	v_pk_add_f32 v[72:73], v[34:35], v[66:67]
	v_pk_add_f32 v[34:35], v[34:35], v[66:67] neg_lo:[0,1] neg_hi:[0,1]
	v_pk_add_f32 v[66:67], v[38:39], v[54:55]
	v_pk_add_f32 v[38:39], v[38:39], v[54:55] neg_lo:[0,1] neg_hi:[0,1]
	v_pk_add_f32 v[76:77], v[72:73], v[66:67]
	v_pk_add_f32 v[54:55], v[72:73], v[66:67] neg_lo:[0,1] neg_hi:[0,1]
	v_pk_add_f32 v[66:67], v[34:35], v[38:39] op_sel:[0,1] op_sel_hi:[1,0] neg_hi:[0,1]
	v_pk_add_f32 v[38:39], v[34:35], v[38:39] op_sel:[0,1] op_sel_hi:[1,0] neg_lo:[0,1]
	v_pk_add_f32 v[34:35], v[48:49], v[68:69]
	v_pk_add_f32 v[68:69], v[48:49], v[68:69] neg_lo:[0,1] neg_hi:[0,1]
	v_pk_add_f32 v[48:49], v[52:53], v[64:65]
	v_pk_add_f32 v[52:53], v[52:53], v[64:65] neg_lo:[0,1] neg_hi:[0,1]
	v_pk_add_f32 v[72:73], v[34:35], v[48:49]
	v_pk_add_f32 v[48:49], v[34:35], v[48:49] neg_lo:[0,1] neg_hi:[0,1]
	v_pk_add_f32 v[74:75], v[68:69], v[52:53] op_sel:[0,1] op_sel_hi:[1,0] neg_hi:[0,1]
	v_pk_add_f32 v[34:35], v[68:69], v[52:53] op_sel:[0,1] op_sel_hi:[1,0] neg_lo:[0,1]
	v_pk_add_f32 v[68:69], v[62:63], v[42:43]
	v_pk_add_f32 v[42:43], v[42:43], v[62:63] neg_lo:[0,1] neg_hi:[0,1]
	v_pk_add_f32 v[52:53], v[70:71], v[80:81]
	v_pk_mul_f32 v[62:63], v[32:33], v[42:43] op_sel:[0,1] op_sel_hi:[0,0] neg_lo:[1,1] neg_hi:[1,0]
	v_pk_fma_f32 v[62:63], v[32:33], v[42:43], v[62:63] op_sel_hi:[0,1,1]
	v_pk_add_f32 v[42:43], v[16:17], v[58:59]
	v_pk_add_f32 v[16:17], v[16:17], v[58:59] neg_lo:[0,1] neg_hi:[0,1]
	v_pk_add_f32 v[64:65], v[70:71], v[80:81] neg_lo:[0,1] neg_hi:[0,1]
	v_xor_b32_e32 v59, 0x80000000, v16
	v_mov_b32_e32 v58, v17
	v_pk_add_f32 v[16:17], v[78:79], v[56:57]
	v_pk_add_f32 v[56:57], v[78:79], v[56:57] neg_lo:[0,1] neg_hi:[0,1]
	s_nop 0
	v_pk_mul_f32 v[70:71], v[32:33], v[56:57] op_sel:[0,1] op_sel_hi:[0,0] neg_lo:[1,1] neg_hi:[1,0]
	v_pk_fma_f32 v[32:33], v[32:33], v[56:57], v[70:71] op_sel_hi:[0,1,1] neg_lo:[1,0,0] neg_hi:[1,0,0]
	v_pk_add_f32 v[56:57], v[52:53], v[42:43]
	v_pk_add_f32 v[42:43], v[52:53], v[42:43] neg_lo:[0,1] neg_hi:[0,1]
	v_pk_add_f32 v[52:53], v[68:69], v[16:17]
	v_pk_add_f32 v[16:17], v[68:69], v[16:17] neg_lo:[0,1] neg_hi:[0,1]
	v_pk_add_f32 v[70:71], v[56:57], v[52:53]
	v_xor_b32_e32 v69, 0x80000000, v16
	v_mov_b32_e32 v68, v17
	v_pk_add_f32 v[56:57], v[56:57], v[52:53] neg_lo:[0,1] neg_hi:[0,1]
	v_pk_add_f32 v[16:17], v[64:65], v[58:59]
	v_pk_add_f32 v[52:53], v[62:63], v[32:33]
	v_pk_add_f32 v[32:33], v[62:63], v[32:33] neg_lo:[0,1] neg_hi:[0,1]
	v_pk_add_f32 v[58:59], v[64:65], v[58:59] neg_lo:[0,1] neg_hi:[0,1]
	v_pk_add_f32 v[64:65], v[16:17], v[52:53]
	v_pk_add_f32 v[52:53], v[16:17], v[52:53] neg_lo:[0,1] neg_hi:[0,1]
	v_mov_b64_e32 v[16:17], s[92:93]
	v_pk_add_f32 v[78:79], v[42:43], v[68:69]
	v_pk_add_f32 v[42:43], v[42:43], v[68:69] neg_lo:[0,1] neg_hi:[0,1]
	v_pk_add_f32 v[68:69], v[58:59], v[32:33] op_sel:[0,1] op_sel_hi:[1,0] neg_hi:[0,1]
	v_pk_add_f32 v[32:33], v[58:59], v[32:33] op_sel:[0,1] op_sel_hi:[1,0] neg_lo:[0,1]
	v_pk_fma_f32 v[58:59], v[10:11], s[42:43], v[16:17] op_sel_hi:[0,1,1]
	ds_write_b64 v13, v[58:59]
	v_pk_fma_f32 v[58:59], v[180:181], s[92:93], v[180:181] op_sel:[1,0,0] op_sel_hi:[0,1,1]
	v_pk_mul_f32 v[62:63], v[58:59], v[76:77] op_sel:[1,1] op_sel_hi:[0,1] neg_lo:[0,1]
	v_pk_fma_f32 v[62:63], v[58:59], v[76:77], v[62:63] op_sel_hi:[1,0,1]
	ds_write_b64 v13, v[62:63] offset:4224
	v_pk_mul_f32 v[62:63], v[180:181], v[58:59] op_sel:[1,1] op_sel_hi:[0,1] neg_lo:[0,1]
	v_pk_fma_f32 v[58:59], v[180:181], v[58:59], v[62:63] op_sel_hi:[1,0,1]
	s_nop 0
	v_pk_mul_f32 v[62:63], v[58:59], v[86:87] op_sel:[1,1] op_sel_hi:[0,1] neg_lo:[0,1]
	v_pk_fma_f32 v[62:63], v[58:59], v[86:87], v[62:63] op_sel_hi:[1,0,1]
	ds_write_b64 v13, v[62:63] offset:8448
	v_pk_mul_f32 v[62:63], v[180:181], v[58:59] op_sel:[1,1] op_sel_hi:[0,1] neg_lo:[0,1]
	v_pk_fma_f32 v[58:59], v[180:181], v[58:59], v[62:63] op_sel_hi:[1,0,1]
	s_nop 0
	v_pk_mul_f32 v[62:63], v[58:59], v[70:71] op_sel:[1,1] op_sel_hi:[0,1] neg_lo:[0,1]
	v_pk_fma_f32 v[62:63], v[58:59], v[70:71], v[62:63] op_sel_hi:[1,0,1]
	ds_write_b64 v13, v[62:63] offset:12672
	v_pk_mul_f32 v[62:63], v[180:181], v[58:59] op_sel:[1,1] op_sel_hi:[0,1] neg_lo:[0,1]
	v_pk_fma_f32 v[58:59], v[180:181], v[58:59], v[62:63] op_sel_hi:[1,0,1]
	s_nop 0
	v_pk_mul_f32 v[62:63], v[60:61], v[58:59] op_sel:[1,1] op_sel_hi:[1,0] neg_lo:[1,0]
	s_nop 0
	v_pk_fma_f32 v[60:61], v[60:61], v[58:59], v[62:63] op_sel_hi:[0,1,1]
	ds_write_b64 v13, v[60:61] offset:16896
	v_pk_mul_f32 v[60:61], v[180:181], v[58:59] op_sel:[1,1] op_sel_hi:[0,1] neg_lo:[0,1]
	v_pk_fma_f32 v[58:59], v[180:181], v[58:59], v[60:61] op_sel_hi:[1,0,1]
	s_nop 0
	v_pk_mul_f32 v[60:61], v[58:59], v[72:73] op_sel:[1,1] op_sel_hi:[0,1] neg_lo:[0,1]
	v_pk_fma_f32 v[60:61], v[58:59], v[72:73], v[60:61] op_sel_hi:[1,0,1]
	ds_write_b64 v13, v[60:61] offset:21120
	v_pk_mul_f32 v[60:61], v[180:181], v[58:59] op_sel:[1,1] op_sel_hi:[0,1] neg_lo:[0,1]
	v_pk_fma_f32 v[58:59], v[180:181], v[58:59], v[60:61] op_sel_hi:[1,0,1]
	s_nop 0
	v_pk_mul_f32 v[60:61], v[82:83], v[58:59] op_sel:[1,1] op_sel_hi:[1,0] neg_lo:[1,0]
	s_nop 0
	v_pk_fma_f32 v[60:61], v[82:83], v[58:59], v[60:61] op_sel_hi:[0,1,1]
	ds_write_b64 v13, v[60:61] offset:25344
	v_pk_mul_f32 v[60:61], v[180:181], v[58:59] op_sel:[1,1] op_sel_hi:[0,1] neg_lo:[0,1]
	v_pk_fma_f32 v[58:59], v[180:181], v[58:59], v[60:61] op_sel_hi:[1,0,1]
	s_nop 0
	v_pk_mul_f32 v[60:61], v[64:65], v[58:59] op_sel:[1,1] op_sel_hi:[1,0] neg_lo:[1,0]
	s_nop 0
	v_pk_fma_f32 v[60:61], v[64:65], v[58:59], v[60:61] op_sel_hi:[0,1,1]
	ds_write_b64 v13, v[60:61] offset:29568
	v_pk_mul_f32 v[60:61], v[180:181], v[58:59] op_sel:[1,1] op_sel_hi:[0,1] neg_lo:[0,1]
	v_pk_fma_f32 v[58:59], v[180:181], v[58:59], v[60:61] op_sel_hi:[1,0,1]
	s_nop 0
	v_pk_mul_f32 v[60:61], v[46:47], v[58:59] op_sel:[1,1] op_sel_hi:[1,0] neg_lo:[1,0]
	s_nop 0
	v_pk_fma_f32 v[46:47], v[46:47], v[58:59], v[60:61] op_sel_hi:[0,1,1]
	ds_write_b64 v13, v[46:47] offset:33792
	v_pk_mul_f32 v[46:47], v[180:181], v[58:59] op_sel:[1,1] op_sel_hi:[0,1] neg_lo:[0,1]
	v_pk_fma_f32 v[46:47], v[180:181], v[58:59], v[46:47] op_sel_hi:[1,0,1]
	s_nop 0
	v_pk_mul_f32 v[58:59], v[66:67], v[46:47] op_sel:[1,1] op_sel_hi:[1,0] neg_lo:[1,0]
	s_nop 0
	v_pk_fma_f32 v[58:59], v[66:67], v[46:47], v[58:59] op_sel_hi:[0,1,1]
	ds_write_b64 v13, v[58:59] offset:38016
	v_pk_mul_f32 v[58:59], v[180:181], v[46:47] op_sel:[1,1] op_sel_hi:[0,1] neg_lo:[0,1]
	v_pk_fma_f32 v[46:47], v[180:181], v[46:47], v[58:59] op_sel_hi:[1,0,1]
	s_nop 0
	v_pk_mul_f32 v[58:59], v[50:51], v[46:47] op_sel:[1,1] op_sel_hi:[1,0] neg_lo:[1,0]
	s_nop 0
	v_pk_fma_f32 v[50:51], v[50:51], v[46:47], v[58:59] op_sel_hi:[0,1,1]
	ds_write_b64 v13, v[50:51] offset:42240
	v_pk_mul_f32 v[50:51], v[180:181], v[46:47] op_sel:[1,1] op_sel_hi:[0,1] neg_lo:[0,1]
	v_pk_fma_f32 v[46:47], v[180:181], v[46:47], v[50:51] op_sel_hi:[1,0,1]
	s_nop 0
	v_pk_mul_f32 v[50:51], v[78:79], v[46:47] op_sel:[1,1] op_sel_hi:[1,0] neg_lo:[1,0]
	s_nop 0
	v_pk_fma_f32 v[50:51], v[78:79], v[46:47], v[50:51] op_sel_hi:[0,1,1]
	ds_write_b64 v13, v[50:51] offset:46464
	v_pk_mul_f32 v[50:51], v[180:181], v[46:47] op_sel:[1,1] op_sel_hi:[0,1] neg_lo:[0,1]
	v_pk_fma_f32 v[46:47], v[180:181], v[46:47], v[50:51] op_sel_hi:[1,0,1]
	s_nop 0
	v_pk_mul_f32 v[50:51], v[40:41], v[46:47] op_sel:[1,1] op_sel_hi:[1,0] neg_lo:[1,0]
	s_nop 0
	v_pk_fma_f32 v[40:41], v[40:41], v[46:47], v[50:51] op_sel_hi:[0,1,1]
	ds_write_b64 v13, v[40:41] offset:50688
	v_pk_mul_f32 v[40:41], v[180:181], v[46:47] op_sel:[1,1] op_sel_hi:[0,1] neg_lo:[0,1]
	v_pk_fma_f32 v[40:41], v[180:181], v[46:47], v[40:41] op_sel_hi:[1,0,1]
	s_nop 0
	v_pk_mul_f32 v[46:47], v[74:75], v[40:41] op_sel:[1,1] op_sel_hi:[1,0] neg_lo:[1,0]
	s_nop 0
	v_pk_fma_f32 v[46:47], v[74:75], v[40:41], v[46:47] op_sel_hi:[0,1,1]
	ds_write_b64 v13, v[46:47] offset:54912
	v_pk_mul_f32 v[46:47], v[180:181], v[40:41] op_sel:[1,1] op_sel_hi:[0,1] neg_lo:[0,1]
	v_pk_fma_f32 v[40:41], v[180:181], v[40:41], v[46:47] op_sel_hi:[1,0,1]
	s_nop 0
	v_pk_mul_f32 v[46:47], v[44:45], v[40:41] op_sel:[1,1] op_sel_hi:[1,0] neg_lo:[1,0]
	s_nop 0
	v_pk_fma_f32 v[44:45], v[44:45], v[40:41], v[46:47] op_sel_hi:[0,1,1]
	ds_write_b64 v13, v[44:45] offset:59136
	v_pk_mul_f32 v[44:45], v[180:181], v[40:41] op_sel:[1,1] op_sel_hi:[0,1] neg_lo:[0,1]
	v_pk_fma_f32 v[40:41], v[180:181], v[40:41], v[44:45] op_sel_hi:[1,0,1]
	s_nop 0
	v_pk_mul_f32 v[44:45], v[68:69], v[40:41] op_sel:[1,1] op_sel_hi:[1,0] neg_lo:[1,0]
	s_nop 0
	v_pk_fma_f32 v[44:45], v[68:69], v[40:41], v[44:45] op_sel_hi:[0,1,1]
	ds_write_b64 v13, v[44:45] offset:63360
	v_pk_mul_f32 v[44:45], v[180:181], v[40:41] op_sel:[1,1] op_sel_hi:[0,1] neg_lo:[0,1]
	v_pk_fma_f32 v[40:41], v[180:181], v[40:41], v[44:45] op_sel_hi:[1,0,1]
	s_mov_b32 s46, s43
	v_sub_f32_e32 v10, v30, v31
	v_pk_mul_f32 v[30:31], v[40:41], s[46:47]
	s_nop 0
	v_pk_fma_f32 v[30:31], v[10:11], v[40:41], v[30:31] op_sel:[0,0,1] op_sel_hi:[0,1,0]
	v_add_u32_e32 v10, 0x10800, v13
	ds_write_b64 v10, v[30:31]
	v_pk_mul_f32 v[30:31], v[180:181], v[40:41] op_sel:[1,1] op_sel_hi:[0,1] neg_lo:[0,1]
	v_pk_fma_f32 v[30:31], v[180:181], v[40:41], v[30:31] op_sel_hi:[1,0,1]
	s_nop 0
	v_pk_mul_f32 v[40:41], v[54:55], v[30:31] op_sel:[1,1] op_sel_hi:[1,0] neg_lo:[1,0]
	v_add_u32_e32 v10, 0x11880, v13
	v_pk_fma_f32 v[40:41], v[54:55], v[30:31], v[40:41] op_sel_hi:[0,1,1]
	ds_write_b64 v10, v[40:41]
	v_pk_mul_f32 v[40:41], v[180:181], v[30:31] op_sel:[1,1] op_sel_hi:[0,1] neg_lo:[0,1]
	v_pk_fma_f32 v[30:31], v[180:181], v[30:31], v[40:41] op_sel_hi:[1,0,1]
	s_nop 0
	v_pk_mul_f32 v[40:41], v[36:37], v[30:31] op_sel:[1,1] op_sel_hi:[1,0] neg_lo:[1,0]
	v_add_u32_e32 v10, 0x12900, v13
	v_pk_fma_f32 v[36:37], v[36:37], v[30:31], v[40:41] op_sel_hi:[0,1,1]
	ds_write_b64 v10, v[36:37]
	v_pk_mul_f32 v[36:37], v[180:181], v[30:31] op_sel:[1,1] op_sel_hi:[0,1] neg_lo:[0,1]
	v_pk_fma_f32 v[30:31], v[180:181], v[30:31], v[36:37] op_sel_hi:[1,0,1]
	s_nop 0
	v_pk_mul_f32 v[36:37], v[56:57], v[30:31] op_sel:[1,1] op_sel_hi:[1,0] neg_lo:[1,0]
	v_add_u32_e32 v10, 0x13980, v13
	v_pk_fma_f32 v[36:37], v[56:57], v[30:31], v[36:37] op_sel_hi:[0,1,1]
	ds_write_b64 v10, v[36:37]
	v_pk_mul_f32 v[36:37], v[180:181], v[30:31] op_sel:[1,1] op_sel_hi:[0,1] neg_lo:[0,1]
	v_pk_fma_f32 v[30:31], v[180:181], v[30:31], v[36:37] op_sel_hi:[1,0,1]
	s_nop 0
	v_pk_mul_f32 v[36:37], v[26:27], v[30:31] op_sel:[1,1] op_sel_hi:[1,0] neg_lo:[1,0]
	v_add_u32_e32 v10, 0x14a00, v13
	v_pk_fma_f32 v[26:27], v[26:27], v[30:31], v[36:37] op_sel_hi:[0,1,1]
	ds_write_b64 v10, v[26:27]
	v_pk_mul_f32 v[26:27], v[180:181], v[30:31] op_sel:[1,1] op_sel_hi:[0,1] neg_lo:[0,1]
	v_pk_fma_f32 v[26:27], v[180:181], v[30:31], v[26:27] op_sel_hi:[1,0,1]
	s_nop 0
	v_pk_mul_f32 v[30:31], v[48:49], v[26:27] op_sel:[1,1] op_sel_hi:[1,0] neg_lo:[1,0]
	v_add_u32_e32 v10, 0x15a80, v13
	v_pk_fma_f32 v[30:31], v[48:49], v[26:27], v[30:31] op_sel_hi:[0,1,1]
	ds_write_b64 v10, v[30:31]
	v_pk_mul_f32 v[30:31], v[180:181], v[26:27] op_sel:[1,1] op_sel_hi:[0,1] neg_lo:[0,1]
	v_pk_fma_f32 v[26:27], v[180:181], v[26:27], v[30:31] op_sel_hi:[1,0,1]
	s_nop 0
	v_pk_mul_f32 v[30:31], v[28:29], v[26:27] op_sel:[1,1] op_sel_hi:[1,0] neg_lo:[1,0]
	v_add_u32_e32 v10, 0x16b00, v13
	v_pk_fma_f32 v[28:29], v[28:29], v[26:27], v[30:31] op_sel_hi:[0,1,1]
	ds_write_b64 v10, v[28:29]
	v_pk_mul_f32 v[28:29], v[180:181], v[26:27] op_sel:[1,1] op_sel_hi:[0,1] neg_lo:[0,1]
	v_pk_fma_f32 v[26:27], v[180:181], v[26:27], v[28:29] op_sel_hi:[1,0,1]
	s_nop 0
	v_pk_mul_f32 v[28:29], v[52:53], v[26:27] op_sel:[1,1] op_sel_hi:[1,0] neg_lo:[1,0]
	v_add_u32_e32 v10, 0x17b80, v13
	v_pk_fma_f32 v[28:29], v[52:53], v[26:27], v[28:29] op_sel_hi:[0,1,1]
	ds_write_b64 v10, v[28:29]
	v_pk_mul_f32 v[28:29], v[180:181], v[26:27] op_sel:[1,1] op_sel_hi:[0,1] neg_lo:[0,1]
	v_pk_fma_f32 v[26:27], v[180:181], v[26:27], v[28:29] op_sel_hi:[1,0,1]
	s_nop 0
	v_pk_mul_f32 v[28:29], v[20:21], v[26:27] op_sel:[1,1] op_sel_hi:[1,0] neg_lo:[1,0]
	v_add_u32_e32 v10, 0x18c00, v13
	v_pk_fma_f32 v[20:21], v[20:21], v[26:27], v[28:29] op_sel_hi:[0,1,1]
	ds_write_b64 v10, v[20:21]
	v_pk_mul_f32 v[20:21], v[180:181], v[26:27] op_sel:[1,1] op_sel_hi:[0,1] neg_lo:[0,1]
	v_pk_fma_f32 v[20:21], v[180:181], v[26:27], v[20:21] op_sel_hi:[1,0,1]
	s_nop 0
	v_pk_mul_f32 v[26:27], v[38:39], v[20:21] op_sel:[1,1] op_sel_hi:[1,0] neg_lo:[1,0]
	v_add_u32_e32 v10, 0x19c80, v13
	v_pk_fma_f32 v[26:27], v[38:39], v[20:21], v[26:27] op_sel_hi:[0,1,1]
	ds_write_b64 v10, v[26:27]
	v_pk_mul_f32 v[26:27], v[180:181], v[20:21] op_sel:[1,1] op_sel_hi:[0,1] neg_lo:[0,1]
	v_pk_fma_f32 v[20:21], v[180:181], v[20:21], v[26:27] op_sel_hi:[1,0,1]
	s_nop 0
	v_pk_mul_f32 v[26:27], v[24:25], v[20:21] op_sel:[1,1] op_sel_hi:[1,0] neg_lo:[1,0]
	v_add_u32_e32 v10, 0x1ad00, v13
	v_pk_fma_f32 v[24:25], v[24:25], v[20:21], v[26:27] op_sel_hi:[0,1,1]
	ds_write_b64 v10, v[24:25]
	v_pk_mul_f32 v[24:25], v[180:181], v[20:21] op_sel:[1,1] op_sel_hi:[0,1] neg_lo:[0,1]
	v_pk_fma_f32 v[20:21], v[180:181], v[20:21], v[24:25] op_sel_hi:[1,0,1]
	s_nop 0
	v_pk_mul_f32 v[24:25], v[42:43], v[20:21] op_sel:[1,1] op_sel_hi:[1,0] neg_lo:[1,0]
	v_add_u32_e32 v10, 0x1bd80, v13
	v_pk_fma_f32 v[24:25], v[42:43], v[20:21], v[24:25] op_sel_hi:[0,1,1]
	ds_write_b64 v10, v[24:25]
	v_pk_mul_f32 v[24:25], v[180:181], v[20:21] op_sel:[1,1] op_sel_hi:[0,1] neg_lo:[0,1]
	v_pk_fma_f32 v[20:21], v[180:181], v[20:21], v[24:25] op_sel_hi:[1,0,1]
	s_nop 0
	v_pk_mul_f32 v[24:25], v[14:15], v[20:21] op_sel:[1,1] op_sel_hi:[1,0] neg_lo:[1,0]
	v_add_u32_e32 v10, 0x1ce00, v13
	v_pk_fma_f32 v[14:15], v[14:15], v[20:21], v[24:25] op_sel_hi:[0,1,1]
	ds_write_b64 v10, v[14:15]
	v_pk_mul_f32 v[14:15], v[180:181], v[20:21] op_sel:[1,1] op_sel_hi:[0,1] neg_lo:[0,1]
	v_pk_fma_f32 v[14:15], v[180:181], v[20:21], v[14:15] op_sel_hi:[1,0,1]
	s_nop 0
	v_pk_mul_f32 v[20:21], v[34:35], v[14:15] op_sel:[1,1] op_sel_hi:[1,0] neg_lo:[1,0]
	v_add_u32_e32 v10, 0x1de80, v13
	v_pk_fma_f32 v[20:21], v[34:35], v[14:15], v[20:21] op_sel_hi:[0,1,1]
	ds_write_b64 v10, v[20:21]
	v_pk_mul_f32 v[20:21], v[180:181], v[14:15] op_sel:[1,1] op_sel_hi:[0,1] neg_lo:[0,1]
	v_pk_fma_f32 v[14:15], v[180:181], v[14:15], v[20:21] op_sel_hi:[1,0,1]
	s_nop 0
	v_pk_mul_f32 v[20:21], v[18:19], v[14:15] op_sel:[1,1] op_sel_hi:[1,0] neg_lo:[1,0]
	v_add_u32_e32 v10, 0x1ef00, v13
	v_pk_fma_f32 v[18:19], v[18:19], v[14:15], v[20:21] op_sel_hi:[0,1,1]
	ds_write_b64 v10, v[18:19]
	v_pk_mul_f32 v[18:19], v[180:181], v[14:15] op_sel:[1,1] op_sel_hi:[0,1] neg_lo:[0,1]
	v_pk_fma_f32 v[14:15], v[180:181], v[14:15], v[18:19] op_sel_hi:[1,0,1]
	s_nop 0
	v_pk_mul_f32 v[18:19], v[32:33], v[14:15] op_sel:[1,1] op_sel_hi:[1,0] neg_lo:[1,0]
	v_add_u32_e32 v10, 0x1ff80, v13
	v_pk_fma_f32 v[14:15], v[32:33], v[14:15], v[18:19] op_sel_hi:[0,1,1]
	ds_write_b64 v10, v[14:15]
	v_mov_b32_e32 v10, v176
	v_mov_b32_e32 v13, v173
	s_waitcnt lgkmcnt(0)
	s_barrier
	v_mov_b32_e32 v14, v182
	v_xad_u32 v30, v13, 3, v10
	v_lshl_add_u32 v73, v30, 3, 0
	v_xad_u32 v30, v13, 4, v10
	v_lshl_add_u32 v72, v30, 3, 0
	v_xad_u32 v30, v13, 5, v10
	v_lshl_add_u32 v71, v30, 3, 0
	v_xad_u32 v30, v13, 6, v10
	v_lshl_add_u32 v70, v30, 3, 0
	v_xad_u32 v30, v13, 7, v10
	v_lshl_add_u32 v69, v30, 3, 0
	v_xad_u32 v30, v13, 8, v10
	v_lshl_add_u32 v30, v30, 3, 0
	v_add_u32_e32 v68, 0x800, v30
	v_xad_u32 v30, v13, 9, v10
	v_lshl_add_u32 v30, v30, 3, 0
	v_add_u32_e32 v67, 0x800, v30
	v_xad_u32 v30, v13, 10, v10
	v_lshl_add_u32 v30, v30, 3, 0
	v_add_u32_e32 v66, 0x800, v30
	v_xad_u32 v30, v13, 11, v10
	v_lshl_add_u32 v30, v30, 3, 0
	v_add_u32_e32 v18, v13, v10
	v_add_u32_e32 v65, 0x800, v30
	v_xad_u32 v30, v13, 12, v10
	v_mov_b32_e32 v15, v183
	v_lshl_add_u32 v76, v18, 3, 0
	v_lshl_add_u32 v30, v30, 3, 0
	ds_read2_b64 v[18:21], v76 offset1:16
	ds_read2_b64 v[40:43], v68 offset1:16
	v_add_u32_e32 v64, 0x800, v30
	v_xad_u32 v30, v13, 13, v10
	v_xad_u32 v22, v13, 1, v10
	v_lshl_add_u32 v30, v30, 3, 0
	v_lshl_add_u32 v75, v22, 3, 0
	v_xad_u32 v26, v13, 2, v10
	v_add_u32_e32 v63, 0x800, v30
	v_xad_u32 v30, v13, 14, v10
	v_xad_u32 v10, v13, 15, v10
	ds_read2_b64 v[22:25], v75 offset0:32 offset1:48
	ds_read2_b64 v[48:51], v67 offset0:32 offset1:48
	v_lshl_add_u32 v30, v30, 3, 0
	v_lshl_add_u32 v10, v10, 3, 0
	v_lshl_add_u32 v74, v26, 3, 0
	v_add_u32_e32 v62, 0x800, v30
	v_add_u32_e32 v13, 0x800, v10
	ds_read2_b64 v[26:29], v74 offset0:64 offset1:80
	ds_read2_b64 v[58:61], v73 offset0:96 offset1:112
	ds_read2_b64 v[78:81], v72 offset0:128 offset1:144
	ds_read2_b64 v[82:85], v71 offset0:160 offset1:176
	ds_read2_b64 v[86:89], v70 offset0:192 offset1:208
	ds_read2_b64 v[90:93], v69 offset0:224 offset1:240
	ds_read2_b64 v[54:57], v66 offset0:64 offset1:80
	ds_read2_b64 v[94:97], v65 offset0:96 offset1:112
	ds_read2_b64 v[98:101], v64 offset0:128 offset1:144
	ds_read2_b64 v[102:105], v63 offset0:160 offset1:176
	ds_read2_b64 v[106:109], v62 offset0:192 offset1:208
	ds_read2_b64 v[110:113], v13 offset0:224 offset1:240
	s_waitcnt lgkmcnt(14)
	v_pk_add_f32 v[114:115], v[18:19], v[40:41]
	v_pk_add_f32 v[40:41], v[18:19], v[40:41] neg_lo:[0,1] neg_hi:[0,1]
	v_pk_add_f32 v[18:19], v[20:21], v[42:43]
	v_pk_add_f32 v[20:21], v[20:21], v[42:43] neg_lo:[0,1] neg_hi:[0,1]
	v_mov_b32_e32 v30, v165
	v_mov_b32_e32 v32, v166
	v_mov_b32_e32 v34, v167
	v_mov_b32_e32 v10, v168
	v_mov_b32_e32 v38, v169
	v_mov_b32_e32 v36, v170
	v_mov_b32_e32 v46, v171
	v_mov_b32_e32 v31, v172
	v_pk_mul_f32 v[42:43], v[20:21], v[46:47] op_sel:[1,0] op_sel_hi:[0,0] neg_lo:[1,1] neg_hi:[0,1]
	s_mov_b32 s14, s43
	v_pk_fma_f32 v[44:45], v[20:21], v[30:31], v[42:43] op_sel_hi:[1,0,1]
	s_waitcnt lgkmcnt(12)
	v_pk_add_f32 v[20:21], v[22:23], v[48:49]
	v_pk_add_f32 v[22:23], v[22:23], v[48:49] neg_lo:[0,1] neg_hi:[0,1]
	s_mov_b32 s15, s42
	v_pk_mul_f32 v[42:43], v[22:23], v[36:37] op_sel:[1,0] op_sel_hi:[0,0] neg_lo:[1,1] neg_hi:[0,1]
	s_nop 0
	v_pk_fma_f32 v[48:49], v[22:23], v[32:33], v[42:43] op_sel_hi:[1,0,1]
	v_pk_add_f32 v[22:23], v[24:25], v[50:51]
	v_pk_add_f32 v[24:25], v[24:25], v[50:51] neg_lo:[0,1] neg_hi:[0,1]
	s_nop 0
	v_pk_mul_f32 v[42:43], v[24:25], v[38:39] op_sel:[1,0] op_sel_hi:[0,0] neg_lo:[1,1] neg_hi:[0,1]
	s_nop 0
	v_pk_fma_f32 v[52:53], v[24:25], v[34:35], v[42:43] op_sel_hi:[1,0,1]
	s_waitcnt lgkmcnt(5)
	v_pk_add_f32 v[24:25], v[26:27], v[54:55]
	v_pk_add_f32 v[26:27], v[26:27], v[54:55] neg_lo:[0,1] neg_hi:[0,1]
	s_nop 0
	v_pk_mul_f32 v[42:43], v[26:27], v[10:11] op_sel:[1,0] op_sel_hi:[0,0] neg_lo:[1,1] neg_hi:[0,1]
	s_nop 0
	v_pk_fma_f32 v[54:55], v[26:27], v[10:11], v[42:43] op_sel_hi:[1,0,1]
	v_pk_add_f32 v[26:27], v[28:29], v[56:57]
	v_pk_add_f32 v[28:29], v[28:29], v[56:57] neg_lo:[0,1] neg_hi:[0,1]
	s_nop 0
	v_pk_mul_f32 v[42:43], v[28:29], v[38:39] op_sel_hi:[1,0]
	s_nop 0
	v_pk_fma_f32 v[56:57], v[28:29], v[34:35], v[42:43] op_sel:[1,0,0] op_sel_hi:[0,0,1] neg_lo:[1,1,0] neg_hi:[0,1,0]
	s_waitcnt lgkmcnt(4)
	v_pk_add_f32 v[42:43], v[58:59], v[94:95] neg_lo:[0,1] neg_hi:[0,1]
	v_pk_add_f32 v[28:29], v[58:59], v[94:95]
	v_pk_mul_f32 v[50:51], v[42:43], v[36:37] op_sel_hi:[1,0]
	s_nop 0
	v_pk_fma_f32 v[58:59], v[42:43], v[32:33], v[50:51] op_sel:[1,0,0] op_sel_hi:[0,0,1] neg_lo:[1,1,0] neg_hi:[0,1,0]
	v_pk_add_f32 v[50:51], v[60:61], v[96:97] neg_lo:[0,1] neg_hi:[0,1]
	v_pk_add_f32 v[42:43], v[60:61], v[96:97]
	v_pk_mul_f32 v[60:61], v[50:51], v[46:47] op_sel_hi:[1,0]
	v_xor_b32_e32 v94, 0x80000000, v51
	v_mov_b32_e32 v95, v50
	s_waitcnt lgkmcnt(3)
	v_pk_add_f32 v[50:51], v[78:79], v[98:99]
	v_pk_add_f32 v[78:79], v[78:79], v[98:99] neg_lo:[0,1] neg_hi:[0,1]
	v_pk_fma_f32 v[60:61], v[94:95], v[30:31], v[60:61] op_sel_hi:[1,0,1] neg_lo:[0,1,0] neg_hi:[0,1,0]
	v_xor_b32_e32 v95, 0x80000000, v78
	v_mov_b32_e32 v94, v79
	v_pk_add_f32 v[78:79], v[80:81], v[100:101]
	v_pk_add_f32 v[80:81], v[80:81], v[100:101] neg_lo:[0,1] neg_hi:[0,1]
	s_nop 0
	v_pk_mul_f32 v[96:97], v[80:81], v[46:47] op_sel_hi:[1,0] neg_lo:[0,1] neg_hi:[0,1]
	s_nop 0
	v_pk_fma_f32 v[80:81], v[80:81], v[30:31], v[96:97] op_sel:[1,0,0] op_sel_hi:[0,0,1] neg_lo:[1,1,0] neg_hi:[0,1,0]
	s_waitcnt lgkmcnt(2)
	v_pk_add_f32 v[96:97], v[82:83], v[102:103]
	v_pk_add_f32 v[82:83], v[82:83], v[102:103] neg_lo:[0,1] neg_hi:[0,1]
	s_nop 0
	v_pk_mul_f32 v[98:99], v[82:83], v[36:37] op_sel_hi:[1,0] neg_lo:[0,1] neg_hi:[0,1]
	s_nop 0
	v_pk_fma_f32 v[82:83], v[82:83], v[32:33], v[98:99] op_sel:[1,0,0] op_sel_hi:[0,0,1] neg_lo:[1,1,0] neg_hi:[0,1,0]
	v_pk_add_f32 v[98:99], v[84:85], v[104:105]
	v_pk_add_f32 v[84:85], v[84:85], v[104:105] neg_lo:[0,1] neg_hi:[0,1]
	s_nop 0
	v_pk_mul_f32 v[100:101], v[84:85], v[38:39] op_sel_hi:[1,0] neg_lo:[0,1] neg_hi:[0,1]
	s_nop 0
	v_pk_fma_f32 v[84:85], v[84:85], v[34:35], v[100:101] op_sel:[1,0,0] op_sel_hi:[0,0,1] neg_lo:[1,1,0] neg_hi:[0,1,0]
	s_waitcnt lgkmcnt(1)
	v_pk_add_f32 v[100:101], v[86:87], v[106:107]
	v_pk_add_f32 v[86:87], v[86:87], v[106:107] neg_lo:[0,1] neg_hi:[0,1]
	s_nop 0
	v_pk_mul_f32 v[102:103], v[86:87], v[10:11] op_sel:[1,0] op_sel_hi:[0,0] neg_lo:[1,1] neg_hi:[0,1]
	s_nop 0
	v_pk_fma_f32 v[86:87], v[86:87], v[10:11], v[102:103] op_sel_hi:[1,0,1] neg_lo:[0,1,0] neg_hi:[0,1,0]
	v_pk_add_f32 v[102:103], v[88:89], v[108:109]
	v_pk_add_f32 v[88:89], v[88:89], v[108:109] neg_lo:[0,1] neg_hi:[0,1]
	s_nop 0
	v_pk_mul_f32 v[38:39], v[88:89], v[38:39] op_sel:[1,0] op_sel_hi:[0,0] neg_lo:[1,1] neg_hi:[0,1]
	s_nop 0
	v_pk_fma_f32 v[88:89], v[88:89], v[34:35], v[38:39] op_sel_hi:[1,0,1] neg_lo:[0,1,0] neg_hi:[0,1,0]
	s_waitcnt lgkmcnt(0)
	v_pk_add_f32 v[38:39], v[90:91], v[110:111] neg_lo:[0,1] neg_hi:[0,1]
	v_pk_add_f32 v[34:35], v[90:91], v[110:111]
	v_pk_mul_f32 v[90:91], v[38:39], v[36:37] op_sel:[1,0] op_sel_hi:[0,0] neg_lo:[1,1] neg_hi:[0,1]
	s_nop 0
	v_pk_fma_f32 v[90:91], v[38:39], v[32:33], v[90:91] op_sel_hi:[1,0,1] neg_lo:[0,1,0] neg_hi:[0,1,0]
	v_pk_add_f32 v[38:39], v[92:93], v[112:113]
	v_pk_add_f32 v[92:93], v[92:93], v[112:113] neg_lo:[0,1] neg_hi:[0,1]
	s_nop 0
	v_pk_mul_f32 v[46:47], v[92:93], v[46:47] op_sel:[1,0] op_sel_hi:[0,0] neg_lo:[1,1] neg_hi:[0,1]
	s_nop 0
	v_pk_fma_f32 v[92:93], v[92:93], v[30:31], v[46:47] op_sel_hi:[1,0,1] neg_lo:[0,1,0] neg_hi:[0,1,0]
	v_pk_add_f32 v[46:47], v[18:19], v[78:79]
	v_pk_add_f32 v[18:19], v[18:19], v[78:79] neg_lo:[0,1] neg_hi:[0,1]
	v_pk_add_f32 v[30:31], v[114:115], v[50:51]
	v_pk_mul_f32 v[78:79], v[18:19], v[36:37] op_sel:[1,0] op_sel_hi:[0,0] neg_lo:[1,1] neg_hi:[0,1]
	v_pk_add_f32 v[50:51], v[114:115], v[50:51] neg_lo:[0,1] neg_hi:[0,1]
	v_pk_fma_f32 v[78:79], v[18:19], v[32:33], v[78:79] op_sel_hi:[1,0,1]
	v_pk_add_f32 v[18:19], v[20:21], v[96:97]
	v_pk_add_f32 v[20:21], v[20:21], v[96:97] neg_lo:[0,1] neg_hi:[0,1]
	s_nop 0
	v_pk_mul_f32 v[96:97], v[20:21], v[10:11] op_sel:[1,0] op_sel_hi:[0,0] neg_lo:[1,1] neg_hi:[0,1]
	s_nop 0
	v_pk_fma_f32 v[20:21], v[20:21], v[10:11], v[96:97] op_sel_hi:[1,0,1]
	v_pk_add_f32 v[96:97], v[22:23], v[98:99]
	v_pk_add_f32 v[22:23], v[22:23], v[98:99] neg_lo:[0,1] neg_hi:[0,1]
	s_nop 0
	v_pk_mul_f32 v[98:99], v[22:23], v[36:37] op_sel_hi:[1,0]
	v_xor_b32_e32 v104, 0x80000000, v23
	v_mov_b32_e32 v105, v22
	v_pk_add_f32 v[22:23], v[24:25], v[100:101]
	v_pk_add_f32 v[24:25], v[24:25], v[100:101] neg_lo:[0,1] neg_hi:[0,1]
	v_pk_fma_f32 v[98:99], v[104:105], v[32:33], v[98:99] op_sel_hi:[1,0,1] neg_lo:[0,1,0] neg_hi:[0,1,0]
	v_xor_b32_e32 v101, 0x80000000, v24
	v_mov_b32_e32 v100, v25
	v_pk_add_f32 v[24:25], v[26:27], v[102:103]
	v_pk_add_f32 v[26:27], v[26:27], v[102:103] neg_lo:[0,1] neg_hi:[0,1]
	s_nop 0
	v_pk_mul_f32 v[102:103], v[26:27], v[36:37] op_sel_hi:[1,0] neg_lo:[0,1] neg_hi:[0,1]
	v_xor_b32_e32 v104, 0x80000000, v27
	v_mov_b32_e32 v105, v26
	v_pk_add_f32 v[26:27], v[28:29], v[34:35]
	v_pk_add_f32 v[28:29], v[28:29], v[34:35] neg_lo:[0,1] neg_hi:[0,1]
	v_pk_fma_f32 v[102:103], v[104:105], v[32:33], v[102:103] op_sel_hi:[1,0,1] neg_lo:[0,1,0] neg_hi:[0,1,0]
	v_pk_mul_f32 v[34:35], v[28:29], v[10:11] op_sel:[1,0] op_sel_hi:[0,0] neg_lo:[1,1] neg_hi:[0,1]
	v_pk_add_f32 v[104:105], v[30:31], v[22:23] neg_lo:[0,1] neg_hi:[0,1]
	v_pk_fma_f32 v[28:29], v[28:29], v[10:11], v[34:35] op_sel_hi:[1,0,1] neg_lo:[0,1,0] neg_hi:[0,1,0]
	v_pk_add_f32 v[34:35], v[42:43], v[38:39]
	v_pk_add_f32 v[38:39], v[42:43], v[38:39] neg_lo:[0,1] neg_hi:[0,1]
	s_nop 0
	v_pk_mul_f32 v[42:43], v[38:39], v[36:37] op_sel:[1,0] op_sel_hi:[0,0] neg_lo:[1,1] neg_hi:[0,1]
	s_nop 0
	v_pk_fma_f32 v[42:43], v[38:39], v[32:33], v[42:43] op_sel_hi:[1,0,1] neg_lo:[0,1,0] neg_hi:[0,1,0]
	v_pk_add_f32 v[38:39], v[30:31], v[22:23]
	v_pk_add_f32 v[22:23], v[46:47], v[24:25]
	v_pk_add_f32 v[24:25], v[46:47], v[24:25] neg_lo:[0,1] neg_hi:[0,1]
	s_nop 0
	v_pk_mul_f32 v[30:31], v[24:25], v[10:11] op_sel:[1,0] op_sel_hi:[0,0] neg_lo:[1,1] neg_hi:[0,1]
	s_nop 0
	v_pk_fma_f32 v[24:25], v[24:25], v[10:11], v[30:31] op_sel_hi:[1,0,1]
	v_pk_add_f32 v[30:31], v[18:19], v[26:27]
	v_pk_add_f32 v[18:19], v[18:19], v[26:27] neg_lo:[0,1] neg_hi:[0,1]
	s_nop 0
	v_xor_b32_e32 v27, 0x80000000, v18
	v_mov_b32_e32 v26, v19
	v_pk_add_f32 v[18:19], v[96:97], v[34:35]
	v_pk_add_f32 v[34:35], v[96:97], v[34:35] neg_lo:[0,1] neg_hi:[0,1]
	s_nop 0
	v_pk_mul_f32 v[46:47], v[34:35], v[10:11] op_sel:[1,0] op_sel_hi:[0,0] neg_lo:[1,1] neg_hi:[0,1]
	s_nop 0
	v_pk_fma_f32 v[34:35], v[34:35], v[10:11], v[46:47] op_sel_hi:[1,0,1] neg_lo:[0,1,0] neg_hi:[0,1,0]
	v_pk_add_f32 v[46:47], v[38:39], v[30:31]
	v_pk_add_f32 v[38:39], v[38:39], v[30:31] neg_lo:[0,1] neg_hi:[0,1]
	v_pk_add_f32 v[30:31], v[22:23], v[18:19]
	v_pk_add_f32 v[18:19], v[22:23], v[18:19] neg_lo:[0,1] neg_hi:[0,1]
	v_pk_add_f32 v[96:97], v[46:47], v[30:31]
	v_xor_b32_e32 v23, 0x80000000, v18
	v_mov_b32_e32 v22, v19
	v_pk_add_f32 v[18:19], v[104:105], v[26:27]
	v_pk_add_f32 v[104:105], v[104:105], v[26:27] neg_lo:[0,1] neg_hi:[0,1]
	v_pk_add_f32 v[26:27], v[24:25], v[34:35]
	v_pk_add_f32 v[24:25], v[24:25], v[34:35] neg_lo:[0,1] neg_hi:[0,1]
	v_pk_add_f32 v[30:31], v[46:47], v[30:31] neg_lo:[0,1] neg_hi:[0,1]
	v_xor_b32_e32 v35, 0x80000000, v24
	v_mov_b32_e32 v34, v25
	v_pk_add_f32 v[24:25], v[50:51], v[100:101]
	v_pk_add_f32 v[100:101], v[50:51], v[100:101] neg_lo:[0,1] neg_hi:[0,1]
	v_pk_add_f32 v[50:51], v[78:79], v[102:103] neg_lo:[0,1] neg_hi:[0,1]
	v_pk_add_f32 v[46:47], v[38:39], v[22:23]
	v_pk_add_f32 v[22:23], v[38:39], v[22:23] neg_lo:[0,1] neg_hi:[0,1]
	v_pk_add_f32 v[106:107], v[18:19], v[26:27]
	v_pk_add_f32 v[26:27], v[18:19], v[26:27] neg_lo:[0,1] neg_hi:[0,1]
	v_pk_add_f32 v[38:39], v[104:105], v[34:35]
	v_pk_add_f32 v[18:19], v[104:105], v[34:35] neg_lo:[0,1] neg_hi:[0,1]
	v_pk_add_f32 v[34:35], v[78:79], v[102:103]
	v_pk_mul_f32 v[78:79], v[10:11], v[50:51] op_sel:[0,1] op_sel_hi:[0,0] neg_lo:[1,1] neg_hi:[1,0]
	v_pk_fma_f32 v[78:79], v[10:11], v[50:51], v[78:79] op_sel_hi:[0,1,1]
	v_pk_add_f32 v[50:51], v[20:21], v[28:29]
	v_pk_add_f32 v[20:21], v[20:21], v[28:29] neg_lo:[0,1] neg_hi:[0,1]
	s_nop 0
	v_xor_b32_e32 v29, 0x80000000, v20
	v_mov_b32_e32 v28, v21
	v_pk_add_f32 v[20:21], v[98:99], v[42:43]
	v_pk_add_f32 v[42:43], v[98:99], v[42:43] neg_lo:[0,1] neg_hi:[0,1]
	s_nop 0
	v_pk_mul_f32 v[98:99], v[10:11], v[42:43] op_sel:[0,1] op_sel_hi:[0,0] neg_lo:[1,1] neg_hi:[1,0]
	v_pk_fma_f32 v[42:43], v[10:11], v[42:43], v[98:99] op_sel_hi:[0,1,1] neg_lo:[1,0,0] neg_hi:[1,0,0]
	v_pk_add_f32 v[98:99], v[24:25], v[50:51]
	v_pk_add_f32 v[24:25], v[24:25], v[50:51] neg_lo:[0,1] neg_hi:[0,1]
	v_pk_add_f32 v[50:51], v[34:35], v[20:21]
	v_pk_add_f32 v[20:21], v[34:35], v[20:21] neg_lo:[0,1] neg_hi:[0,1]
	v_pk_add_f32 v[104:105], v[98:99], v[50:51]
	v_xor_b32_e32 v103, 0x80000000, v20
	v_mov_b32_e32 v102, v21
	v_pk_add_f32 v[34:35], v[98:99], v[50:51] neg_lo:[0,1] neg_hi:[0,1]
	v_pk_add_f32 v[20:21], v[100:101], v[28:29]
	v_pk_add_f32 v[98:99], v[100:101], v[28:29] neg_lo:[0,1] neg_hi:[0,1]
	v_pk_add_f32 v[28:29], v[78:79], v[42:43]
	v_pk_add_f32 v[42:43], v[78:79], v[42:43] neg_lo:[0,1] neg_hi:[0,1]
	v_pk_add_f32 v[100:101], v[20:21], v[28:29]
	v_xor_b32_e32 v79, 0x80000000, v42
	v_mov_b32_e32 v78, v43
	v_pk_add_f32 v[28:29], v[20:21], v[28:29] neg_lo:[0,1] neg_hi:[0,1]
	v_pk_add_f32 v[42:43], v[98:99], v[78:79]
	v_pk_add_f32 v[20:21], v[98:99], v[78:79] neg_lo:[0,1] neg_hi:[0,1]
	v_pk_add_f32 v[78:79], v[40:41], v[94:95]
	v_pk_add_f32 v[94:95], v[40:41], v[94:95] neg_lo:[0,1] neg_hi:[0,1]
	v_pk_add_f32 v[40:41], v[44:45], v[80:81]
	v_pk_add_f32 v[44:45], v[44:45], v[80:81] neg_lo:[0,1] neg_hi:[0,1]
	v_pk_add_f32 v[50:51], v[24:25], v[102:103]
	v_pk_mul_f32 v[80:81], v[36:37], v[44:45] op_sel:[0,1] op_sel_hi:[0,0] neg_lo:[1,1] neg_hi:[1,0]
	v_pk_fma_f32 v[44:45], v[32:33], v[44:45], v[80:81] op_sel_hi:[0,1,1]
	v_pk_add_f32 v[80:81], v[48:49], v[82:83]
	v_pk_add_f32 v[48:49], v[48:49], v[82:83] neg_lo:[0,1] neg_hi:[0,1]
	v_pk_add_f32 v[24:25], v[24:25], v[102:103] neg_lo:[0,1] neg_hi:[0,1]
	v_pk_mul_f32 v[82:83], v[10:11], v[48:49] op_sel:[0,1] op_sel_hi:[0,0] neg_lo:[1,1] neg_hi:[1,0]
	v_pk_fma_f32 v[82:83], v[10:11], v[48:49], v[82:83] op_sel_hi:[0,1,1]
	v_pk_add_f32 v[48:49], v[52:53], v[84:85]
	v_pk_add_f32 v[52:53], v[52:53], v[84:85] neg_lo:[0,1] neg_hi:[0,1]
	s_nop 0
	v_pk_mul_f32 v[84:85], v[32:33], v[52:53] op_sel:[0,1] op_sel_hi:[0,0] neg_lo:[1,1] neg_hi:[1,0]
	v_pk_fma_f32 v[52:53], v[36:37], v[52:53], v[84:85] op_sel_hi:[0,1,1]
	v_pk_add_f32 v[84:85], v[54:55], v[86:87]
	v_pk_add_f32 v[54:55], v[54:55], v[86:87] neg_lo:[0,1] neg_hi:[0,1]
	s_nop 0
	v_xor_b32_e32 v87, 0x80000000, v54
	v_mov_b32_e32 v86, v55
	v_pk_add_f32 v[54:55], v[56:57], v[88:89]
	v_pk_add_f32 v[56:57], v[56:57], v[88:89] neg_lo:[0,1] neg_hi:[0,1]
	s_nop 0
	v_pk_mul_f32 v[88:89], v[32:33], v[56:57] op_sel:[0,1] op_sel_hi:[0,0] neg_lo:[1,1] neg_hi:[1,0]
	v_pk_fma_f32 v[56:57], v[36:37], v[56:57], v[88:89] op_sel_hi:[0,1,1] neg_lo:[1,0,0] neg_hi:[1,0,0]
	v_pk_add_f32 v[88:89], v[58:59], v[90:91]
	v_pk_add_f32 v[58:59], v[58:59], v[90:91] neg_lo:[0,1] neg_hi:[0,1]
	s_nop 0
	v_pk_mul_f32 v[90:91], v[10:11], v[58:59] op_sel:[0,1] op_sel_hi:[0,0] neg_lo:[1,1] neg_hi:[1,0]
	v_pk_fma_f32 v[58:59], v[10:11], v[58:59], v[90:91] op_sel_hi:[0,1,1] neg_lo:[1,0,0] neg_hi:[1,0,0]
	v_pk_add_f32 v[90:91], v[60:61], v[92:93]
	v_pk_add_f32 v[60:61], v[60:61], v[92:93] neg_lo:[0,1] neg_hi:[0,1]
	s_nop 0
	v_pk_mul_f32 v[36:37], v[36:37], v[60:61] op_sel:[0,1] op_sel_hi:[0,0] neg_lo:[1,1] neg_hi:[1,0]
	v_pk_fma_f32 v[36:37], v[32:33], v[60:61], v[36:37] op_sel_hi:[0,1,1] neg_lo:[1,0,0] neg_hi:[1,0,0]
	v_pk_add_f32 v[32:33], v[78:79], v[84:85]
	v_pk_add_f32 v[60:61], v[78:79], v[84:85] neg_lo:[0,1] neg_hi:[0,1]
	v_pk_add_f32 v[78:79], v[54:55], v[40:41]
	v_pk_add_f32 v[40:41], v[40:41], v[54:55] neg_lo:[0,1] neg_hi:[0,1]
	s_nop 0
	v_pk_mul_f32 v[54:55], v[10:11], v[40:41] op_sel:[0,1] op_sel_hi:[0,0] neg_lo:[1,1] neg_hi:[1,0]
	v_pk_fma_f32 v[54:55], v[10:11], v[40:41], v[54:55] op_sel_hi:[0,1,1]
	v_pk_add_f32 v[40:41], v[80:81], v[88:89]
	v_pk_add_f32 v[80:81], v[80:81], v[88:89] neg_lo:[0,1] neg_hi:[0,1]
	s_nop 0
	v_xor_b32_e32 v85, 0x80000000, v80
	v_mov_b32_e32 v84, v81
	v_pk_add_f32 v[80:81], v[48:49], v[90:91]
	v_pk_add_f32 v[48:49], v[48:49], v[90:91] neg_lo:[0,1] neg_hi:[0,1]
	v_pk_add_f32 v[90:91], v[78:79], v[80:81]
	v_pk_mul_f32 v[88:89], v[10:11], v[48:49] op_sel:[0,1] op_sel_hi:[0,0] neg_lo:[1,1] neg_hi:[1,0]
	v_pk_fma_f32 v[48:49], v[10:11], v[48:49], v[88:89] op_sel_hi:[0,1,1] neg_lo:[1,0,0] neg_hi:[1,0,0]
	v_pk_add_f32 v[88:89], v[32:33], v[40:41]
	v_pk_add_f32 v[32:33], v[32:33], v[40:41] neg_lo:[0,1] neg_hi:[0,1]
	v_pk_add_f32 v[40:41], v[78:79], v[80:81] neg_lo:[0,1] neg_hi:[0,1]
	v_pk_add_f32 v[80:81], v[88:89], v[90:91] neg_lo:[0,1] neg_hi:[0,1]
	v_pk_add_f32 v[92:93], v[32:33], v[40:41] op_sel:[0,1] op_sel_hi:[1,0] neg_hi:[0,1]
	v_pk_add_f32 v[40:41], v[32:33], v[40:41] op_sel:[0,1] op_sel_hi:[1,0] neg_lo:[0,1]
	v_pk_add_f32 v[78:79], v[54:55], v[48:49]
	v_pk_add_f32 v[48:49], v[54:55], v[48:49] neg_lo:[0,1] neg_hi:[0,1]
	v_pk_add_f32 v[32:33], v[60:61], v[84:85]
	v_pk_add_f32 v[60:61], v[60:61], v[84:85] neg_lo:[0,1] neg_hi:[0,1]
	v_xor_b32_e32 v55, 0x80000000, v48
	v_mov_b32_e32 v54, v49
	v_pk_add_f32 v[84:85], v[32:33], v[78:79]
	v_pk_add_f32 v[48:49], v[32:33], v[78:79] neg_lo:[0,1] neg_hi:[0,1]
	v_pk_add_f32 v[78:79], v[60:61], v[54:55]
	v_pk_add_f32 v[32:33], v[60:61], v[54:55] neg_lo:[0,1] neg_hi:[0,1]
	v_pk_add_f32 v[54:55], v[94:95], v[86:87]
	v_pk_add_f32 v[60:61], v[94:95], v[86:87] neg_lo:[0,1] neg_hi:[0,1]
	v_pk_add_f32 v[86:87], v[56:57], v[44:45]
	v_pk_add_f32 v[44:45], v[44:45], v[56:57] neg_lo:[0,1] neg_hi:[0,1]
	v_pk_add_f32 v[88:89], v[88:89], v[90:91]
	v_pk_mul_f32 v[56:57], v[10:11], v[44:45] op_sel:[0,1] op_sel_hi:[0,0] neg_lo:[1,1] neg_hi:[1,0]
	v_pk_fma_f32 v[56:57], v[10:11], v[44:45], v[56:57] op_sel_hi:[0,1,1]
	v_pk_add_f32 v[44:45], v[82:83], v[58:59]
	v_pk_add_f32 v[58:59], v[82:83], v[58:59] neg_lo:[0,1] neg_hi:[0,1]
	s_nop 0
	v_xor_b32_e32 v83, 0x80000000, v58
	v_mov_b32_e32 v82, v59
	v_pk_add_f32 v[58:59], v[52:53], v[36:37]
	v_pk_add_f32 v[36:37], v[52:53], v[36:37] neg_lo:[0,1] neg_hi:[0,1]
	s_nop 0
	v_pk_mul_f32 v[52:53], v[10:11], v[36:37] op_sel:[0,1] op_sel_hi:[0,0] neg_lo:[1,1] neg_hi:[1,0]
	v_pk_fma_f32 v[36:37], v[10:11], v[36:37], v[52:53] op_sel_hi:[0,1,1] neg_lo:[1,0,0] neg_hi:[1,0,0]
	v_pk_add_f32 v[52:53], v[54:55], v[44:45]
	v_pk_add_f32 v[44:45], v[54:55], v[44:45] neg_lo:[0,1] neg_hi:[0,1]
	v_pk_add_f32 v[54:55], v[86:87], v[58:59]
	v_pk_add_f32 v[58:59], v[86:87], v[58:59] neg_lo:[0,1] neg_hi:[0,1]
	s_nop 0
	v_xor_b32_e32 v87, 0x80000000, v58
	v_mov_b32_e32 v86, v59
	v_pk_add_f32 v[58:59], v[52:53], v[54:55]
	v_pk_add_f32 v[54:55], v[52:53], v[54:55] neg_lo:[0,1] neg_hi:[0,1]
	v_pk_add_f32 v[52:53], v[60:61], v[82:83]
	v_pk_add_f32 v[60:61], v[60:61], v[82:83] neg_lo:[0,1] neg_hi:[0,1]
	v_pk_add_f32 v[82:83], v[56:57], v[36:37]
	v_pk_add_f32 v[36:37], v[56:57], v[36:37] neg_lo:[0,1] neg_hi:[0,1]
	v_pk_add_f32 v[94:95], v[44:45], v[86:87]
	v_pk_add_f32 v[44:45], v[44:45], v[86:87] neg_lo:[0,1] neg_hi:[0,1]
	v_pk_add_f32 v[86:87], v[52:53], v[82:83]
	v_pk_add_f32 v[52:53], v[52:53], v[82:83] neg_lo:[0,1] neg_hi:[0,1]
	v_pk_add_f32 v[82:83], v[60:61], v[36:37] op_sel:[0,1] op_sel_hi:[1,0] neg_hi:[0,1]
	v_pk_add_f32 v[36:37], v[60:61], v[36:37] op_sel:[0,1] op_sel_hi:[1,0] neg_lo:[0,1]
	v_pk_fma_f32 v[60:61], v[14:15], s[92:93], v[14:15] op_sel:[1,0,0] op_sel_hi:[0,1,1]
	v_pk_mul_f32 v[56:57], v[96:97], s[14:15] op_sel:[1,0] neg_lo:[1,0]
	v_pk_mul_f32 v[90:91], v[60:61], v[88:89] op_sel:[1,1] op_sel_hi:[0,1] neg_lo:[0,1]
	v_pk_fma_f32 v[56:57], v[96:97], s[42:43], v[56:57] op_sel_hi:[0,1,1]
	v_pk_fma_f32 v[88:89], v[60:61], v[88:89], v[90:91] op_sel_hi:[1,0,1]
	ds_write2_b64 v76, v[56:57], v[88:89] offset1:16
	v_pk_mul_f32 v[56:57], v[14:15], v[60:61] op_sel:[1,1] op_sel_hi:[0,1] neg_lo:[0,1]
	v_pk_fma_f32 v[56:57], v[14:15], v[60:61], v[56:57] op_sel_hi:[1,0,1]
	s_nop 0
	v_pk_mul_f32 v[60:61], v[56:57], v[104:105] op_sel:[1,1] op_sel_hi:[0,1] neg_lo:[0,1]
	v_pk_mul_f32 v[76:77], v[14:15], v[56:57] op_sel:[1,1] op_sel_hi:[0,1] neg_lo:[0,1]
	v_pk_fma_f32 v[60:61], v[56:57], v[104:105], v[60:61] op_sel_hi:[1,0,1]
	v_pk_fma_f32 v[56:57], v[14:15], v[56:57], v[76:77] op_sel_hi:[1,0,1]
	s_nop 0
	v_pk_mul_f32 v[76:77], v[56:57], v[58:59] op_sel:[1,1] op_sel_hi:[0,1] neg_lo:[0,1]
	v_pk_fma_f32 v[58:59], v[56:57], v[58:59], v[76:77] op_sel_hi:[1,0,1]
	ds_write2_b64 v75, v[60:61], v[58:59] offset0:32 offset1:48
	v_pk_mul_f32 v[58:59], v[14:15], v[56:57] op_sel:[1,1] op_sel_hi:[0,1] neg_lo:[0,1]
	v_pk_fma_f32 v[56:57], v[14:15], v[56:57], v[58:59] op_sel_hi:[1,0,1]
	s_nop 0
	v_pk_mul_f32 v[58:59], v[56:57], v[106:107] op_sel:[1,1] op_sel_hi:[0,1] neg_lo:[0,1]
	v_pk_mul_f32 v[60:61], v[14:15], v[56:57] op_sel:[1,1] op_sel_hi:[0,1] neg_lo:[0,1]
	v_pk_fma_f32 v[58:59], v[56:57], v[106:107], v[58:59] op_sel_hi:[1,0,1]
	v_pk_fma_f32 v[56:57], v[14:15], v[56:57], v[60:61] op_sel_hi:[1,0,1]
	s_nop 0
	v_pk_mul_f32 v[60:61], v[56:57], v[84:85] op_sel:[1,1] op_sel_hi:[0,1] neg_lo:[0,1]
	v_pk_fma_f32 v[60:61], v[56:57], v[84:85], v[60:61] op_sel_hi:[1,0,1]
	ds_write2_b64 v74, v[58:59], v[60:61] offset0:64 offset1:80
	v_pk_mul_f32 v[58:59], v[14:15], v[56:57] op_sel:[1,1] op_sel_hi:[0,1] neg_lo:[0,1]
	v_pk_fma_f32 v[56:57], v[14:15], v[56:57], v[58:59] op_sel_hi:[1,0,1]
	s_nop 0
	v_pk_mul_f32 v[58:59], v[56:57], v[100:101] op_sel:[1,1] op_sel_hi:[0,1] neg_lo:[0,1]
	v_pk_mul_f32 v[60:61], v[14:15], v[56:57] op_sel:[1,1] op_sel_hi:[0,1] neg_lo:[0,1]
	v_pk_fma_f32 v[58:59], v[56:57], v[100:101], v[58:59] op_sel_hi:[1,0,1]
	v_pk_fma_f32 v[56:57], v[14:15], v[56:57], v[60:61] op_sel_hi:[1,0,1]
	s_nop 0
	v_pk_mul_f32 v[60:61], v[56:57], v[86:87] op_sel:[1,1] op_sel_hi:[0,1] neg_lo:[0,1]
	v_pk_fma_f32 v[60:61], v[56:57], v[86:87], v[60:61] op_sel_hi:[1,0,1]
	ds_write2_b64 v73, v[58:59], v[60:61] offset0:96 offset1:112
	v_pk_mul_f32 v[58:59], v[14:15], v[56:57] op_sel:[1,1] op_sel_hi:[0,1] neg_lo:[0,1]
	v_pk_fma_f32 v[56:57], v[14:15], v[56:57], v[58:59] op_sel_hi:[1,0,1]
	s_nop 0
	v_pk_mul_f32 v[58:59], v[56:57], v[46:47] op_sel:[1,1] op_sel_hi:[0,1] neg_lo:[0,1]
	v_pk_fma_f32 v[46:47], v[56:57], v[46:47], v[58:59] op_sel_hi:[1,0,1]
	v_pk_mul_f32 v[58:59], v[14:15], v[56:57] op_sel:[1,1] op_sel_hi:[0,1] neg_lo:[0,1]
	v_pk_fma_f32 v[56:57], v[14:15], v[56:57], v[58:59] op_sel_hi:[1,0,1]
	s_nop 0
	v_pk_mul_f32 v[58:59], v[56:57], v[92:93] op_sel:[1,1] op_sel_hi:[0,1] neg_lo:[0,1]
	v_pk_fma_f32 v[58:59], v[56:57], v[92:93], v[58:59] op_sel_hi:[1,0,1]
	ds_write2_b64 v72, v[46:47], v[58:59] offset0:128 offset1:144
	v_pk_mul_f32 v[46:47], v[14:15], v[56:57] op_sel:[1,1] op_sel_hi:[0,1] neg_lo:[0,1]
	v_pk_fma_f32 v[46:47], v[14:15], v[56:57], v[46:47] op_sel_hi:[1,0,1]
	s_nop 0
	v_pk_mul_f32 v[56:57], v[46:47], v[50:51] op_sel:[1,1] op_sel_hi:[0,1] neg_lo:[0,1]
	v_pk_fma_f32 v[50:51], v[46:47], v[50:51], v[56:57] op_sel_hi:[1,0,1]
	v_pk_mul_f32 v[56:57], v[14:15], v[46:47] op_sel:[1,1] op_sel_hi:[0,1] neg_lo:[0,1]
	v_pk_fma_f32 v[46:47], v[14:15], v[46:47], v[56:57] op_sel_hi:[1,0,1]
	s_nop 0
	v_pk_mul_f32 v[56:57], v[46:47], v[94:95] op_sel:[1,1] op_sel_hi:[0,1] neg_lo:[0,1]
	v_pk_fma_f32 v[56:57], v[46:47], v[94:95], v[56:57] op_sel_hi:[1,0,1]
	ds_write2_b64 v71, v[50:51], v[56:57] offset0:160 offset1:176
	v_pk_mul_f32 v[50:51], v[14:15], v[46:47] op_sel:[1,1] op_sel_hi:[0,1] neg_lo:[0,1]
	v_pk_fma_f32 v[46:47], v[14:15], v[46:47], v[50:51] op_sel_hi:[1,0,1]
	s_nop 0
	v_pk_mul_f32 v[50:51], v[38:39], v[46:47] op_sel:[1,1] op_sel_hi:[1,0] neg_lo:[1,0]
	s_nop 0
	v_pk_fma_f32 v[38:39], v[38:39], v[46:47], v[50:51] op_sel_hi:[0,1,1]
	v_pk_mul_f32 v[50:51], v[14:15], v[46:47] op_sel:[1,1] op_sel_hi:[0,1] neg_lo:[0,1]
	v_pk_fma_f32 v[46:47], v[14:15], v[46:47], v[50:51] op_sel_hi:[1,0,1]
	s_nop 0
	v_pk_mul_f32 v[50:51], v[46:47], v[78:79] op_sel:[1,1] op_sel_hi:[0,1] neg_lo:[0,1]
	v_pk_fma_f32 v[50:51], v[46:47], v[78:79], v[50:51] op_sel_hi:[1,0,1]
	ds_write2_b64 v70, v[38:39], v[50:51] offset0:192 offset1:208
	v_pk_mul_f32 v[38:39], v[14:15], v[46:47] op_sel:[1,1] op_sel_hi:[0,1] neg_lo:[0,1]
	v_pk_fma_f32 v[38:39], v[14:15], v[46:47], v[38:39] op_sel_hi:[1,0,1]
	s_nop 0
	v_pk_mul_f32 v[46:47], v[42:43], v[38:39] op_sel:[1,1] op_sel_hi:[1,0] neg_lo:[1,0]
	s_nop 0
	v_pk_fma_f32 v[42:43], v[42:43], v[38:39], v[46:47] op_sel_hi:[0,1,1]
	v_pk_mul_f32 v[46:47], v[14:15], v[38:39] op_sel:[1,1] op_sel_hi:[0,1] neg_lo:[0,1]
	v_pk_fma_f32 v[38:39], v[14:15], v[38:39], v[46:47] op_sel_hi:[1,0,1]
	s_nop 0
	v_pk_mul_f32 v[46:47], v[38:39], v[82:83] op_sel:[1,1] op_sel_hi:[0,1] neg_lo:[0,1]
	v_pk_fma_f32 v[46:47], v[38:39], v[82:83], v[46:47] op_sel_hi:[1,0,1]
	ds_write2_b64 v69, v[42:43], v[46:47] offset0:224 offset1:240
	v_pk_mul_f32 v[42:43], v[14:15], v[38:39] op_sel:[1,1] op_sel_hi:[0,1] neg_lo:[0,1]
	v_pk_fma_f32 v[38:39], v[14:15], v[38:39], v[42:43] op_sel_hi:[1,0,1]
	s_nop 0
	v_pk_mul_f32 v[42:43], v[30:31], v[38:39] op_sel:[1,1] op_sel_hi:[1,0] neg_lo:[1,0]
	s_nop 0
	v_pk_fma_f32 v[30:31], v[30:31], v[38:39], v[42:43] op_sel_hi:[0,1,1]
	v_pk_mul_f32 v[42:43], v[14:15], v[38:39] op_sel:[1,1] op_sel_hi:[0,1] neg_lo:[0,1]
	v_pk_fma_f32 v[38:39], v[14:15], v[38:39], v[42:43] op_sel_hi:[1,0,1]
	s_nop 0
	v_pk_mul_f32 v[42:43], v[80:81], v[38:39] op_sel:[1,1] op_sel_hi:[1,0] neg_lo:[1,0]
	s_nop 0
	v_pk_fma_f32 v[42:43], v[80:81], v[38:39], v[42:43] op_sel_hi:[0,1,1]
	ds_write2_b64 v68, v[30:31], v[42:43] offset1:16
	v_pk_mul_f32 v[30:31], v[14:15], v[38:39] op_sel:[1,1] op_sel_hi:[0,1] neg_lo:[0,1]
	v_pk_fma_f32 v[30:31], v[14:15], v[38:39], v[30:31] op_sel_hi:[1,0,1]
	s_nop 0
	v_pk_mul_f32 v[38:39], v[34:35], v[30:31] op_sel:[1,1] op_sel_hi:[1,0] neg_lo:[1,0]
	s_nop 0
	v_pk_fma_f32 v[34:35], v[34:35], v[30:31], v[38:39] op_sel_hi:[0,1,1]
	v_pk_mul_f32 v[38:39], v[14:15], v[30:31] op_sel:[1,1] op_sel_hi:[0,1] neg_lo:[0,1]
	v_pk_fma_f32 v[30:31], v[14:15], v[30:31], v[38:39] op_sel_hi:[1,0,1]
	s_nop 0
	v_pk_mul_f32 v[38:39], v[54:55], v[30:31] op_sel:[1,1] op_sel_hi:[1,0] neg_lo:[1,0]
	s_nop 0
	v_pk_fma_f32 v[38:39], v[54:55], v[30:31], v[38:39] op_sel_hi:[0,1,1]
	ds_write2_b64 v67, v[34:35], v[38:39] offset0:32 offset1:48
	v_pk_mul_f32 v[34:35], v[14:15], v[30:31] op_sel:[1,1] op_sel_hi:[0,1] neg_lo:[0,1]
	v_pk_fma_f32 v[30:31], v[14:15], v[30:31], v[34:35] op_sel_hi:[1,0,1]
	s_nop 0
	v_pk_mul_f32 v[34:35], v[26:27], v[30:31] op_sel:[1,1] op_sel_hi:[1,0] neg_lo:[1,0]
	s_nop 0
	v_pk_fma_f32 v[26:27], v[26:27], v[30:31], v[34:35] op_sel_hi:[0,1,1]
	v_pk_mul_f32 v[34:35], v[14:15], v[30:31] op_sel:[1,1] op_sel_hi:[0,1] neg_lo:[0,1]
	v_pk_fma_f32 v[30:31], v[14:15], v[30:31], v[34:35] op_sel_hi:[1,0,1]
	s_nop 0
	v_pk_mul_f32 v[34:35], v[48:49], v[30:31] op_sel:[1,1] op_sel_hi:[1,0] neg_lo:[1,0]
	s_nop 0
	v_pk_fma_f32 v[34:35], v[48:49], v[30:31], v[34:35] op_sel_hi:[0,1,1]
	ds_write2_b64 v66, v[26:27], v[34:35] offset0:64 offset1:80
	v_pk_mul_f32 v[26:27], v[14:15], v[30:31] op_sel:[1,1] op_sel_hi:[0,1] neg_lo:[0,1]
	v_pk_fma_f32 v[26:27], v[14:15], v[30:31], v[26:27] op_sel_hi:[1,0,1]
	s_nop 0
	v_pk_mul_f32 v[30:31], v[28:29], v[26:27] op_sel:[1,1] op_sel_hi:[1,0] neg_lo:[1,0]
	s_nop 0
	v_pk_fma_f32 v[28:29], v[28:29], v[26:27], v[30:31] op_sel_hi:[0,1,1]
	v_pk_mul_f32 v[30:31], v[14:15], v[26:27] op_sel:[1,1] op_sel_hi:[0,1] neg_lo:[0,1]
	v_pk_fma_f32 v[26:27], v[14:15], v[26:27], v[30:31] op_sel_hi:[1,0,1]
	s_nop 0
	v_pk_mul_f32 v[30:31], v[52:53], v[26:27] op_sel:[1,1] op_sel_hi:[1,0] neg_lo:[1,0]
	s_nop 0
	v_pk_fma_f32 v[30:31], v[52:53], v[26:27], v[30:31] op_sel_hi:[0,1,1]
	ds_write2_b64 v65, v[28:29], v[30:31] offset0:96 offset1:112
	v_pk_mul_f32 v[28:29], v[14:15], v[26:27] op_sel:[1,1] op_sel_hi:[0,1] neg_lo:[0,1]
	v_pk_fma_f32 v[26:27], v[14:15], v[26:27], v[28:29] op_sel_hi:[1,0,1]
	s_nop 0
	v_pk_mul_f32 v[28:29], v[22:23], v[26:27] op_sel:[1,1] op_sel_hi:[1,0] neg_lo:[1,0]
	s_nop 0
	v_pk_fma_f32 v[22:23], v[22:23], v[26:27], v[28:29] op_sel_hi:[0,1,1]
	v_pk_mul_f32 v[28:29], v[14:15], v[26:27] op_sel:[1,1] op_sel_hi:[0,1] neg_lo:[0,1]
	v_pk_fma_f32 v[26:27], v[14:15], v[26:27], v[28:29] op_sel_hi:[1,0,1]
	s_nop 0
	v_pk_mul_f32 v[28:29], v[40:41], v[26:27] op_sel:[1,1] op_sel_hi:[1,0] neg_lo:[1,0]
	s_nop 0
	v_pk_fma_f32 v[28:29], v[40:41], v[26:27], v[28:29] op_sel_hi:[0,1,1]
	ds_write2_b64 v64, v[22:23], v[28:29] offset0:128 offset1:144
	v_pk_mul_f32 v[22:23], v[14:15], v[26:27] op_sel:[1,1] op_sel_hi:[0,1] neg_lo:[0,1]
	v_pk_fma_f32 v[22:23], v[14:15], v[26:27], v[22:23] op_sel_hi:[1,0,1]
	s_nop 0
	v_pk_mul_f32 v[26:27], v[24:25], v[22:23] op_sel:[1,1] op_sel_hi:[1,0] neg_lo:[1,0]
	s_nop 0
	v_pk_fma_f32 v[24:25], v[24:25], v[22:23], v[26:27] op_sel_hi:[0,1,1]
	v_pk_mul_f32 v[26:27], v[14:15], v[22:23] op_sel:[1,1] op_sel_hi:[0,1] neg_lo:[0,1]
	v_pk_fma_f32 v[22:23], v[14:15], v[22:23], v[26:27] op_sel_hi:[1,0,1]
	s_nop 0
	v_pk_mul_f32 v[26:27], v[44:45], v[22:23] op_sel:[1,1] op_sel_hi:[1,0] neg_lo:[1,0]
	s_nop 0
	v_pk_fma_f32 v[26:27], v[44:45], v[22:23], v[26:27] op_sel_hi:[0,1,1]
	ds_write2_b64 v63, v[24:25], v[26:27] offset0:160 offset1:176
	v_pk_mul_f32 v[24:25], v[14:15], v[22:23] op_sel:[1,1] op_sel_hi:[0,1] neg_lo:[0,1]
	v_pk_fma_f32 v[22:23], v[14:15], v[22:23], v[24:25] op_sel_hi:[1,0,1]
	s_nop 0
	v_pk_mul_f32 v[24:25], v[18:19], v[22:23] op_sel:[1,1] op_sel_hi:[1,0] neg_lo:[1,0]
	s_nop 0
	v_pk_fma_f32 v[18:19], v[18:19], v[22:23], v[24:25] op_sel_hi:[0,1,1]
	v_pk_mul_f32 v[24:25], v[14:15], v[22:23] op_sel:[1,1] op_sel_hi:[0,1] neg_lo:[0,1]
	v_pk_fma_f32 v[22:23], v[14:15], v[22:23], v[24:25] op_sel_hi:[1,0,1]
	s_nop 0
	v_pk_mul_f32 v[24:25], v[32:33], v[22:23] op_sel:[1,1] op_sel_hi:[1,0] neg_lo:[1,0]
	s_nop 0
	v_pk_fma_f32 v[24:25], v[32:33], v[22:23], v[24:25] op_sel_hi:[0,1,1]
	ds_write2_b64 v62, v[18:19], v[24:25] offset0:192 offset1:208
	v_pk_mul_f32 v[18:19], v[14:15], v[22:23] op_sel:[1,1] op_sel_hi:[0,1] neg_lo:[0,1]
	v_pk_fma_f32 v[18:19], v[14:15], v[22:23], v[18:19] op_sel_hi:[1,0,1]
	s_nop 0
	v_pk_mul_f32 v[22:23], v[20:21], v[18:19] op_sel:[1,1] op_sel_hi:[1,0] neg_lo:[1,0]
	s_nop 0
	v_pk_fma_f32 v[20:21], v[20:21], v[18:19], v[22:23] op_sel_hi:[0,1,1]
	v_pk_mul_f32 v[22:23], v[14:15], v[18:19] op_sel:[1,1] op_sel_hi:[0,1] neg_lo:[0,1]
	v_pk_fma_f32 v[14:15], v[14:15], v[18:19], v[22:23] op_sel_hi:[1,0,1]
	s_nop 0
	v_pk_mul_f32 v[18:19], v[36:37], v[14:15] op_sel:[1,1] op_sel_hi:[1,0] neg_lo:[1,0]
	s_nop 0
	v_pk_fma_f32 v[14:15], v[36:37], v[14:15], v[18:19] op_sel_hi:[0,1,1]
	ds_write2_b64 v13, v[20:21], v[14:15] offset0:224 offset1:240
	v_mov_b32_e32 v14, v1
	v_mov_b32_e32 v10, v178
	v_mov_b32_e32 v13, v177
	s_waitcnt lgkmcnt(0)
	s_barrier
	v_mov_b32_e32 v50, v168
	v_xor_b32_e32 v18, 1, v13
	v_lshlrev_b32_e32 v10, 3, v10
	v_lshlrev_b32_e32 v18, 3, v18
	v_add3_u32 v20, 0, v18, v10
	v_xor_b32_e32 v18, 2, v13
	v_lshlrev_b32_e32 v18, 3, v18
	v_xor_b32_e32 v26, 5, v13
	v_add3_u32 v22, 0, v18, v10
	v_xor_b32_e32 v18, 3, v13
	v_lshlrev_b32_e32 v26, 3, v26
	v_lshlrev_b32_e32 v15, 3, v13
	v_lshlrev_b32_e32 v18, 3, v18
	v_add3_u32 v28, 0, v26, v10
	v_xor_b32_e32 v26, 6, v13
	v_add3_u32 v15, 0, v15, v10
	v_add3_u32 v24, 0, v18, v10
	v_lshlrev_b32_e32 v26, 3, v26
	v_xor_b32_e32 v34, 9, v13
	ds_read_b64 v[18:19], v15
	ds_read_b64 v[20:21], v20
	ds_read_b64 v[22:23], v22
	ds_read_b64 v[24:25], v24
	v_xor_b32_e32 v15, 4, v13
	v_add3_u32 v30, 0, v26, v10
	v_xor_b32_e32 v26, 7, v13
	v_lshlrev_b32_e32 v34, 3, v34
	v_lshlrev_b32_e32 v15, 3, v15
	v_lshlrev_b32_e32 v26, 3, v26
	v_add3_u32 v36, 0, v34, v10
	v_xor_b32_e32 v34, 10, v13
	v_add3_u32 v15, 0, v15, v10
	v_add3_u32 v32, 0, v26, v10
	v_lshlrev_b32_e32 v34, 3, v34
	ds_read_b64 v[26:27], v15
	ds_read_b64 v[28:29], v28
	ds_read_b64 v[30:31], v30
	ds_read_b64 v[32:33], v32
	v_xor_b32_e32 v15, 8, v13
	v_add3_u32 v38, 0, v34, v10
	v_xor_b32_e32 v34, 11, v13
	v_lshlrev_b32_e32 v15, 3, v15
	v_lshlrev_b32_e32 v34, 3, v34
	v_xor_b32_e32 v42, 13, v13
	v_add3_u32 v15, 0, v15, v10
	v_add3_u32 v40, 0, v34, v10
	v_lshlrev_b32_e32 v42, 3, v42
	ds_read_b64 v[34:35], v15
	ds_read_b64 v[36:37], v36
	ds_read_b64 v[38:39], v38
	ds_read_b64 v[40:41], v40
	v_xor_b32_e32 v15, 12, v13
	v_add3_u32 v44, 0, v42, v10
	v_xor_b32_e32 v42, 14, v13
	v_xor_b32_e32 v13, 15, v13
	v_lshlrev_b32_e32 v15, 3, v15
	v_lshlrev_b32_e32 v42, 3, v42
	v_lshlrev_b32_e32 v13, 3, v13
	v_add3_u32 v15, 0, v15, v10
	v_add3_u32 v46, 0, v42, v10
	v_add3_u32 v10, 0, v13, v10
	ds_read_b64 v[42:43], v15
	ds_read_b64 v[44:45], v44
	ds_read_b64 v[46:47], v46
	ds_read_b64 v[48:49], v10
	s_waitcnt lgkmcnt(7)
	v_pk_add_f32 v[54:55], v[18:19], v[34:35]
	v_mov_b32_e32 v10, v166
	v_pk_add_f32 v[18:19], v[18:19], v[34:35] neg_lo:[0,1] neg_hi:[0,1]
	s_waitcnt lgkmcnt(6)
	v_pk_add_f32 v[34:35], v[20:21], v[36:37]
	v_pk_add_f32 v[20:21], v[20:21], v[36:37] neg_lo:[0,1] neg_hi:[0,1]
	v_mov_b32_e32 v52, v170
	v_ashrrev_i32_e32 v15, 31, v14
	v_pk_mul_f32 v[36:37], v[20:21], v[52:53] op_sel:[1,0] op_sel_hi:[0,0] neg_lo:[1,1] neg_hi:[0,1]
	v_pk_fma_f32 v[20:21], v[20:21], v[10:11], v[36:37] op_sel_hi:[1,0,1]
	s_waitcnt lgkmcnt(5)
	v_pk_add_f32 v[36:37], v[22:23], v[38:39]
	v_pk_add_f32 v[22:23], v[22:23], v[38:39] neg_lo:[0,1] neg_hi:[0,1]
	s_movk_i32 s85, 0x1000
	v_pk_mul_f32 v[38:39], v[22:23], v[50:51] op_sel:[1,0] op_sel_hi:[0,0] neg_lo:[1,1] neg_hi:[0,1]
	v_pk_fma_f32 v[22:23], v[22:23], v[50:51], v[38:39] op_sel_hi:[1,0,1]
	s_waitcnt lgkmcnt(4)
	v_pk_add_f32 v[38:39], v[24:25], v[40:41]
	v_pk_add_f32 v[24:25], v[24:25], v[40:41] neg_lo:[0,1] neg_hi:[0,1]
	s_movk_i32 s84, 0x2000
	v_pk_mul_f32 v[40:41], v[24:25], v[52:53] op_sel_hi:[1,0]
	s_nop 0
	v_pk_fma_f32 v[24:25], v[24:25], v[10:11], v[40:41] op_sel:[1,0,0] op_sel_hi:[0,0,1] neg_lo:[1,1,0] neg_hi:[0,1,0]
	s_waitcnt lgkmcnt(3)
	v_pk_add_f32 v[40:41], v[26:27], v[42:43]
	v_pk_add_f32 v[26:27], v[26:27], v[42:43] neg_lo:[0,1] neg_hi:[0,1]
	v_mov_b32_e32 v13, v177
	v_xor_b32_e32 v43, 0x80000000, v26
	v_mov_b32_e32 v42, v27
	s_waitcnt lgkmcnt(2)
	v_pk_add_f32 v[26:27], v[28:29], v[44:45]
	v_pk_add_f32 v[28:29], v[28:29], v[44:45] neg_lo:[0,1] neg_hi:[0,1]
	s_movk_i32 s88, 0x6000
	v_pk_mul_f32 v[44:45], v[28:29], v[52:53] op_sel_hi:[1,0] neg_lo:[0,1] neg_hi:[0,1]
	s_nop 0
	v_pk_fma_f32 v[28:29], v[28:29], v[10:11], v[44:45] op_sel:[1,0,0] op_sel_hi:[0,0,1] neg_lo:[1,1,0] neg_hi:[0,1,0]
	s_waitcnt lgkmcnt(1)
	v_pk_add_f32 v[44:45], v[30:31], v[46:47]
	v_pk_add_f32 v[30:31], v[30:31], v[46:47] neg_lo:[0,1] neg_hi:[0,1]
	s_mov_b32 s0, 0x8000
	v_pk_mul_f32 v[46:47], v[30:31], v[50:51] op_sel:[1,0] op_sel_hi:[0,0] neg_lo:[1,1] neg_hi:[0,1]
	s_movk_i32 s86, 0x5000
	v_pk_fma_f32 v[30:31], v[30:31], v[50:51], v[46:47] op_sel_hi:[1,0,1] neg_lo:[0,1,0] neg_hi:[0,1,0]
	s_waitcnt lgkmcnt(0)
	v_pk_add_f32 v[46:47], v[32:33], v[48:49]
	v_pk_add_f32 v[32:33], v[32:33], v[48:49] neg_lo:[0,1] neg_hi:[0,1]
	v_mov_b32_e32 v72, v165
	v_pk_mul_f32 v[48:49], v[32:33], v[52:53] op_sel:[1,0] op_sel_hi:[0,0] neg_lo:[1,1] neg_hi:[0,1]
	v_pk_add_f32 v[52:53], v[34:35], v[26:27]
	v_pk_add_f32 v[26:27], v[34:35], v[26:27] neg_lo:[0,1] neg_hi:[0,1]
	v_pk_fma_f32 v[32:33], v[32:33], v[10:11], v[48:49] op_sel_hi:[1,0,1] neg_lo:[0,1,0] neg_hi:[0,1,0]
	v_pk_mul_f32 v[34:35], v[26:27], v[50:51] op_sel:[1,0] op_sel_hi:[0,0] neg_lo:[1,1] neg_hi:[0,1]
	v_pk_add_f32 v[48:49], v[54:55], v[40:41]
	v_pk_fma_f32 v[26:27], v[26:27], v[50:51], v[34:35] op_sel_hi:[1,0,1]
	v_pk_add_f32 v[34:35], v[36:37], v[44:45]
	v_pk_add_f32 v[36:37], v[36:37], v[44:45] neg_lo:[0,1] neg_hi:[0,1]
	v_pk_add_f32 v[40:41], v[54:55], v[40:41] neg_lo:[0,1] neg_hi:[0,1]
	v_xor_b32_e32 v45, 0x80000000, v36
	v_mov_b32_e32 v44, v37
	v_pk_add_f32 v[36:37], v[38:39], v[46:47]
	v_pk_add_f32 v[38:39], v[38:39], v[46:47] neg_lo:[0,1] neg_hi:[0,1]
	v_mov_b32_e32 v10, v179
	v_pk_mul_f32 v[46:47], v[38:39], v[50:51] op_sel:[1,0] op_sel_hi:[0,0] neg_lo:[1,1] neg_hi:[0,1]
	v_mov_b32_e32 v74, v167
	v_pk_fma_f32 v[38:39], v[38:39], v[50:51], v[46:47] op_sel_hi:[1,0,1] neg_lo:[0,1,0] neg_hi:[0,1,0]
	v_pk_add_f32 v[46:47], v[48:49], v[34:35]
	v_pk_add_f32 v[34:35], v[48:49], v[34:35] neg_lo:[0,1] neg_hi:[0,1]
	v_pk_add_f32 v[48:49], v[52:53], v[36:37]
	v_pk_add_f32 v[36:37], v[52:53], v[36:37] neg_lo:[0,1] neg_hi:[0,1]
	v_mov_b32_e32 v76, v169
	v_xor_b32_e32 v53, 0x80000000, v36
	v_mov_b32_e32 v52, v37
	v_pk_add_f32 v[36:37], v[46:47], v[48:49]
	v_pk_add_f32 v[46:47], v[46:47], v[48:49] neg_lo:[0,1] neg_hi:[0,1]
	v_pk_add_f32 v[48:49], v[34:35], v[52:53]
	v_pk_add_f32 v[34:35], v[34:35], v[52:53] neg_lo:[0,1] neg_hi:[0,1]
	v_pk_add_f32 v[52:53], v[40:41], v[44:45]
	v_pk_add_f32 v[40:41], v[40:41], v[44:45] neg_lo:[0,1] neg_hi:[0,1]
	v_pk_add_f32 v[44:45], v[26:27], v[38:39]
	v_pk_add_f32 v[26:27], v[26:27], v[38:39] neg_lo:[0,1] neg_hi:[0,1]
	v_mov_b32_e32 v78, v171
	v_xor_b32_e32 v39, 0x80000000, v26
	v_mov_b32_e32 v38, v27
	v_pk_add_f32 v[26:27], v[52:53], v[44:45]
	v_pk_add_f32 v[44:45], v[52:53], v[44:45] neg_lo:[0,1] neg_hi:[0,1]
	v_pk_add_f32 v[52:53], v[40:41], v[38:39]
	v_pk_add_f32 v[38:39], v[40:41], v[38:39] neg_lo:[0,1] neg_hi:[0,1]
	v_pk_add_f32 v[40:41], v[18:19], v[42:43]
	v_pk_add_f32 v[18:19], v[18:19], v[42:43] neg_lo:[0,1] neg_hi:[0,1]
	v_pk_add_f32 v[42:43], v[20:21], v[28:29]
	v_pk_add_f32 v[20:21], v[20:21], v[28:29] neg_lo:[0,1] neg_hi:[0,1]
	v_mov_b32_e32 v83, v11
	v_pk_mul_f32 v[28:29], v[50:51], v[20:21] op_sel:[0,1] op_sel_hi:[0,0] neg_lo:[1,1] neg_hi:[1,0]
	v_pk_fma_f32 v[20:21], v[50:51], v[20:21], v[28:29] op_sel_hi:[0,1,1]
	v_pk_add_f32 v[28:29], v[22:23], v[30:31]
	v_pk_add_f32 v[22:23], v[22:23], v[30:31] neg_lo:[0,1] neg_hi:[0,1]
	s_mov_b32 s1, 0xe000
	v_xor_b32_e32 v31, 0x80000000, v22
	v_mov_b32_e32 v30, v23
	v_pk_add_f32 v[22:23], v[24:25], v[32:33]
	v_pk_add_f32 v[24:25], v[24:25], v[32:33] neg_lo:[0,1] neg_hi:[0,1]
	s_mov_b32 s8, 0x8000
	v_pk_mul_f32 v[32:33], v[50:51], v[24:25] op_sel:[0,1] op_sel_hi:[0,0] neg_lo:[1,1] neg_hi:[1,0]
	v_pk_fma_f32 v[24:25], v[50:51], v[24:25], v[32:33] op_sel_hi:[0,1,1] neg_lo:[1,0,0] neg_hi:[1,0,0]
	v_pk_add_f32 v[32:33], v[40:41], v[28:29]
	v_pk_add_f32 v[28:29], v[40:41], v[28:29] neg_lo:[0,1] neg_hi:[0,1]
	v_pk_add_f32 v[40:41], v[42:43], v[22:23]
	v_pk_add_f32 v[22:23], v[42:43], v[22:23] neg_lo:[0,1] neg_hi:[0,1]
	v_mov_b32_e32 v50, v168
	v_xor_b32_e32 v43, 0x80000000, v22
	v_mov_b32_e32 v42, v23
	v_pk_add_f32 v[22:23], v[32:33], v[40:41]
	v_pk_add_f32 v[32:33], v[32:33], v[40:41] neg_lo:[0,1] neg_hi:[0,1]
	v_pk_add_f32 v[40:41], v[28:29], v[42:43]
	v_pk_add_f32 v[28:29], v[28:29], v[42:43] neg_lo:[0,1] neg_hi:[0,1]
	v_pk_add_f32 v[42:43], v[18:19], v[30:31]
	v_pk_add_f32 v[18:19], v[18:19], v[30:31] neg_lo:[0,1] neg_hi:[0,1]
	v_pk_add_f32 v[30:31], v[20:21], v[24:25]
	v_pk_add_f32 v[20:21], v[20:21], v[24:25] neg_lo:[0,1] neg_hi:[0,1]
	s_mov_b32 s7, 0xa000
	v_xor_b32_e32 v25, 0x80000000, v20
	v_mov_b32_e32 v24, v21
	v_pk_add_f32 v[20:21], v[42:43], v[30:31]
	v_pk_add_f32 v[30:31], v[42:43], v[30:31] neg_lo:[0,1] neg_hi:[0,1]
	v_pk_add_f32 v[42:43], v[18:19], v[24:25]
	v_pk_add_f32 v[18:19], v[18:19], v[24:25] neg_lo:[0,1] neg_hi:[0,1]
	v_lshl_add_u64 v[24:25], v[14:15], 3, s[48:49]
	global_store_dwordx2 v[24:25], v[36:37], off
	v_add_u32_e32 v24, 0x200, v14
	v_ashrrev_i32_e32 v25, 31, v24
	v_lshl_add_u64 v[24:25], v[24:25], 3, s[48:49]
	global_store_dwordx2 v[24:25], v[22:23], off
	v_add_u32_e32 v22, 0x400, v14
	v_ashrrev_i32_e32 v23, 31, v22
	v_lshl_add_u64 v[22:23], v[22:23], 3, s[48:49]
	global_store_dwordx2 v[22:23], v[26:27], off
	v_add_u32_e32 v22, 0x600, v14
	v_ashrrev_i32_e32 v23, 31, v22
	v_lshl_add_u64 v[22:23], v[22:23], 3, s[48:49]
	global_store_dwordx2 v[22:23], v[20:21], off
	v_add_u32_e32 v20, 0x800, v14
	v_ashrrev_i32_e32 v21, 31, v20
	v_lshl_add_u64 v[20:21], v[20:21], 3, s[48:49]
	global_store_dwordx2 v[20:21], v[48:49], off
	v_add_u32_e32 v20, 0xa00, v14
	v_ashrrev_i32_e32 v21, 31, v20
	v_lshl_add_u64 v[20:21], v[20:21], 3, s[48:49]
	global_store_dwordx2 v[20:21], v[40:41], off
	v_add_u32_e32 v20, 0xc00, v14
	v_ashrrev_i32_e32 v21, 31, v20
	v_lshl_add_u64 v[20:21], v[20:21], 3, s[48:49]
	global_store_dwordx2 v[20:21], v[52:53], off
	v_add_u32_e32 v20, 0xe00, v14
	v_ashrrev_i32_e32 v21, 31, v20
	v_lshl_add_u64 v[20:21], v[20:21], 3, s[48:49]
	global_store_dwordx2 v[20:21], v[42:43], off
	v_add_u32_e32 v20, 0x1000, v14
	v_ashrrev_i32_e32 v21, 31, v20
	v_lshl_add_u64 v[20:21], v[20:21], 3, s[48:49]
	global_store_dwordx2 v[20:21], v[46:47], off
	v_add_u32_e32 v20, 0x1200, v14
	v_ashrrev_i32_e32 v21, 31, v20
	v_lshl_add_u64 v[20:21], v[20:21], 3, s[48:49]
	global_store_dwordx2 v[20:21], v[32:33], off
	v_add_u32_e32 v20, 0x1400, v14
	v_ashrrev_i32_e32 v21, 31, v20
	v_lshl_add_u64 v[20:21], v[20:21], 3, s[48:49]
	global_store_dwordx2 v[20:21], v[44:45], off
	v_add_u32_e32 v20, 0x1600, v14
	v_ashrrev_i32_e32 v21, 31, v20
	v_lshl_add_u64 v[20:21], v[20:21], 3, s[48:49]
	global_store_dwordx2 v[20:21], v[30:31], off
	v_add_u32_e32 v20, 0x1800, v14
	v_ashrrev_i32_e32 v21, 31, v20
	v_lshl_add_u64 v[20:21], v[20:21], 3, s[48:49]
	global_store_dwordx2 v[20:21], v[34:35], off
	v_add_u32_e32 v20, 0x1a00, v14
	v_ashrrev_i32_e32 v21, 31, v20
	v_lshl_add_u64 v[20:21], v[20:21], 3, s[48:49]
	global_store_dwordx2 v[20:21], v[28:29], off
	v_add_u32_e32 v20, 0x1c00, v14
	v_ashrrev_i32_e32 v21, 31, v20
	v_lshl_add_u64 v[20:21], v[20:21], 3, s[48:49]
	global_store_dwordx2 v[20:21], v[38:39], off
	v_add_u32_e32 v20, 0x1e00, v14
	v_ashrrev_i32_e32 v21, 31, v20
	v_lshl_add_u64 v[20:21], v[20:21], 3, s[48:49]
	global_store_dwordx2 v[20:21], v[18:19], off
	v_mov_b32_e32 v52, v170
	v_xor_b32_e32 v18, 1, v13
	v_lshlrev_b32_e32 v10, 3, v10
	v_lshlrev_b32_e32 v18, 3, v18
	v_add3_u32 v20, 0, v18, v10
	v_xor_b32_e32 v18, 2, v13
	v_lshlrev_b32_e32 v18, 3, v18
	v_xor_b32_e32 v26, 5, v13
	v_add3_u32 v22, 0, v18, v10
	v_xor_b32_e32 v18, 3, v13
	v_lshlrev_b32_e32 v26, 3, v26
	v_lshlrev_b32_e32 v15, 3, v13
	v_lshlrev_b32_e32 v18, 3, v18
	v_add3_u32 v28, 0, v26, v10
	v_xor_b32_e32 v26, 6, v13
	v_add3_u32 v15, 0, v15, v10
	v_add3_u32 v24, 0, v18, v10
	v_lshlrev_b32_e32 v26, 3, v26
	v_xor_b32_e32 v34, 9, v13
	ds_read_b64 v[18:19], v15
	ds_read_b64 v[20:21], v20
	ds_read_b64 v[22:23], v22
	ds_read_b64 v[24:25], v24
	v_xor_b32_e32 v15, 4, v13
	v_add3_u32 v30, 0, v26, v10
	v_xor_b32_e32 v26, 7, v13
	v_lshlrev_b32_e32 v34, 3, v34
	v_lshlrev_b32_e32 v15, 3, v15
	v_lshlrev_b32_e32 v26, 3, v26
	v_add3_u32 v36, 0, v34, v10
	v_xor_b32_e32 v34, 10, v13
	v_add3_u32 v15, 0, v15, v10
	v_add3_u32 v32, 0, v26, v10
	v_lshlrev_b32_e32 v34, 3, v34
	ds_read_b64 v[26:27], v15
	ds_read_b64 v[28:29], v28
	ds_read_b64 v[30:31], v30
	ds_read_b64 v[32:33], v32
	v_xor_b32_e32 v15, 8, v13
	v_add3_u32 v38, 0, v34, v10
	v_xor_b32_e32 v34, 11, v13
	v_lshlrev_b32_e32 v15, 3, v15
	v_lshlrev_b32_e32 v34, 3, v34
	v_xor_b32_e32 v42, 13, v13
	v_add3_u32 v15, 0, v15, v10
	v_add3_u32 v40, 0, v34, v10
	v_lshlrev_b32_e32 v42, 3, v42
	ds_read_b64 v[34:35], v15
	ds_read_b64 v[36:37], v36
	ds_read_b64 v[38:39], v38
	ds_read_b64 v[40:41], v40
	v_xor_b32_e32 v15, 12, v13
	v_add3_u32 v44, 0, v42, v10
	v_xor_b32_e32 v42, 14, v13
	v_xor_b32_e32 v13, 15, v13
	v_lshlrev_b32_e32 v15, 3, v15
	v_lshlrev_b32_e32 v42, 3, v42
	v_lshlrev_b32_e32 v13, 3, v13
	v_add3_u32 v15, 0, v15, v10
	v_add3_u32 v46, 0, v42, v10
	v_add3_u32 v10, 0, v13, v10
	ds_read_b64 v[42:43], v15
	ds_read_b64 v[44:45], v44
	ds_read_b64 v[46:47], v46
	ds_read_b64 v[48:49], v10
	s_waitcnt lgkmcnt(7)
	v_pk_add_f32 v[54:55], v[18:19], v[34:35]
	v_mov_b32_e32 v10, v166
	v_pk_add_f32 v[18:19], v[18:19], v[34:35] neg_lo:[0,1] neg_hi:[0,1]
	s_waitcnt lgkmcnt(6)
	v_pk_add_f32 v[34:35], v[20:21], v[36:37]
	v_pk_add_f32 v[20:21], v[20:21], v[36:37] neg_lo:[0,1] neg_hi:[0,1]
	s_mov_b32 s9, 0x9000
	v_pk_mul_f32 v[36:37], v[20:21], v[52:53] op_sel:[1,0] op_sel_hi:[0,0] neg_lo:[1,1] neg_hi:[0,1]
	v_pk_fma_f32 v[20:21], v[20:21], v[10:11], v[36:37] op_sel_hi:[1,0,1]
	s_waitcnt lgkmcnt(5)
	v_pk_add_f32 v[36:37], v[22:23], v[38:39]
	v_pk_add_f32 v[22:23], v[22:23], v[38:39] neg_lo:[0,1] neg_hi:[0,1]
	s_mov_b32 s5, 0xb000
	v_pk_mul_f32 v[38:39], v[22:23], v[50:51] op_sel:[1,0] op_sel_hi:[0,0] neg_lo:[1,1] neg_hi:[0,1]
	v_pk_fma_f32 v[22:23], v[22:23], v[50:51], v[38:39] op_sel_hi:[1,0,1]
	s_waitcnt lgkmcnt(4)
	v_pk_add_f32 v[38:39], v[24:25], v[40:41]
	v_pk_add_f32 v[24:25], v[24:25], v[40:41] neg_lo:[0,1] neg_hi:[0,1]
	s_mov_b32 s6, 0xc000
	v_pk_mul_f32 v[40:41], v[24:25], v[52:53] op_sel_hi:[1,0]
	s_nop 0
	v_pk_fma_f32 v[24:25], v[24:25], v[10:11], v[40:41] op_sel:[1,0,0] op_sel_hi:[0,0,1] neg_lo:[1,1,0] neg_hi:[0,1,0]
	s_waitcnt lgkmcnt(3)
	v_pk_add_f32 v[40:41], v[26:27], v[42:43]
	v_pk_add_f32 v[26:27], v[26:27], v[42:43] neg_lo:[0,1] neg_hi:[0,1]
	s_mov_b32 s4, 0xd000
	v_xor_b32_e32 v43, 0x80000000, v26
	v_mov_b32_e32 v42, v27
	s_waitcnt lgkmcnt(2)
	v_pk_add_f32 v[26:27], v[28:29], v[44:45]
	v_pk_add_f32 v[28:29], v[28:29], v[44:45] neg_lo:[0,1] neg_hi:[0,1]
	s_nop 0
	v_pk_mul_f32 v[44:45], v[28:29], v[52:53] op_sel_hi:[1,0] neg_lo:[0,1] neg_hi:[0,1]
	s_nop 0
	v_pk_fma_f32 v[28:29], v[28:29], v[10:11], v[44:45] op_sel:[1,0,0] op_sel_hi:[0,0,1] neg_lo:[1,1,0] neg_hi:[0,1,0]
	s_waitcnt lgkmcnt(1)
	v_pk_add_f32 v[44:45], v[30:31], v[46:47]
	v_pk_add_f32 v[30:31], v[30:31], v[46:47] neg_lo:[0,1] neg_hi:[0,1]
	s_nop 0
	v_pk_mul_f32 v[46:47], v[30:31], v[50:51] op_sel:[1,0] op_sel_hi:[0,0] neg_lo:[1,1] neg_hi:[0,1]
	s_nop 0
	v_pk_fma_f32 v[30:31], v[30:31], v[50:51], v[46:47] op_sel_hi:[1,0,1] neg_lo:[0,1,0] neg_hi:[0,1,0]
	s_waitcnt lgkmcnt(0)
	v_pk_add_f32 v[46:47], v[32:33], v[48:49]
	v_pk_add_f32 v[32:33], v[32:33], v[48:49] neg_lo:[0,1] neg_hi:[0,1]
	s_nop 0
	v_pk_mul_f32 v[48:49], v[32:33], v[52:53] op_sel:[1,0] op_sel_hi:[0,0] neg_lo:[1,1] neg_hi:[0,1]
	v_pk_add_f32 v[52:53], v[34:35], v[26:27]
	v_pk_add_f32 v[26:27], v[34:35], v[26:27] neg_lo:[0,1] neg_hi:[0,1]
	v_pk_fma_f32 v[32:33], v[32:33], v[10:11], v[48:49] op_sel_hi:[1,0,1] neg_lo:[0,1,0] neg_hi:[0,1,0]
	v_pk_mul_f32 v[34:35], v[26:27], v[50:51] op_sel:[1,0] op_sel_hi:[0,0] neg_lo:[1,1] neg_hi:[0,1]
	v_pk_add_f32 v[48:49], v[54:55], v[40:41]
	v_pk_fma_f32 v[26:27], v[26:27], v[50:51], v[34:35] op_sel_hi:[1,0,1]
	v_pk_add_f32 v[34:35], v[36:37], v[44:45]
	v_pk_add_f32 v[36:37], v[36:37], v[44:45] neg_lo:[0,1] neg_hi:[0,1]
	v_pk_add_f32 v[40:41], v[54:55], v[40:41] neg_lo:[0,1] neg_hi:[0,1]
	v_xor_b32_e32 v45, 0x80000000, v36
	v_mov_b32_e32 v44, v37
	v_pk_add_f32 v[36:37], v[38:39], v[46:47]
	v_pk_add_f32 v[38:39], v[38:39], v[46:47] neg_lo:[0,1] neg_hi:[0,1]
	v_pk_mul_f32 v[46:47], v[38:39], v[50:51] op_sel:[1,0] op_sel_hi:[0,0] neg_lo:[1,1] neg_hi:[0,1]
	s_nop 0
	v_pk_fma_f32 v[38:39], v[38:39], v[50:51], v[46:47] op_sel_hi:[1,0,1] neg_lo:[0,1,0] neg_hi:[0,1,0]
	v_pk_add_f32 v[46:47], v[48:49], v[34:35]
	v_pk_add_f32 v[34:35], v[48:49], v[34:35] neg_lo:[0,1] neg_hi:[0,1]
	v_pk_add_f32 v[48:49], v[52:53], v[36:37]
	v_pk_add_f32 v[36:37], v[52:53], v[36:37] neg_lo:[0,1] neg_hi:[0,1]
	s_nop 0
	v_xor_b32_e32 v53, 0x80000000, v36
	v_mov_b32_e32 v52, v37
	v_pk_add_f32 v[36:37], v[46:47], v[48:49]
	v_pk_add_f32 v[46:47], v[46:47], v[48:49] neg_lo:[0,1] neg_hi:[0,1]
	v_pk_add_f32 v[48:49], v[34:35], v[52:53]
	v_pk_add_f32 v[34:35], v[34:35], v[52:53] neg_lo:[0,1] neg_hi:[0,1]
	v_pk_add_f32 v[52:53], v[40:41], v[44:45]
	v_pk_add_f32 v[40:41], v[40:41], v[44:45] neg_lo:[0,1] neg_hi:[0,1]
	v_pk_add_f32 v[44:45], v[26:27], v[38:39]
	v_pk_add_f32 v[26:27], v[26:27], v[38:39] neg_lo:[0,1] neg_hi:[0,1]
	s_nop 0
	v_xor_b32_e32 v39, 0x80000000, v26
	v_mov_b32_e32 v38, v27
	v_pk_add_f32 v[26:27], v[52:53], v[44:45]
	v_pk_add_f32 v[44:45], v[52:53], v[44:45] neg_lo:[0,1] neg_hi:[0,1]
	v_pk_add_f32 v[52:53], v[40:41], v[38:39]
	v_pk_add_f32 v[38:39], v[40:41], v[38:39] neg_lo:[0,1] neg_hi:[0,1]
	v_pk_add_f32 v[40:41], v[18:19], v[42:43]
	v_pk_add_f32 v[18:19], v[18:19], v[42:43] neg_lo:[0,1] neg_hi:[0,1]
	v_pk_add_f32 v[42:43], v[20:21], v[28:29]
	v_pk_add_f32 v[20:21], v[20:21], v[28:29] neg_lo:[0,1] neg_hi:[0,1]
	s_nop 0
	v_pk_mul_f32 v[28:29], v[50:51], v[20:21] op_sel:[0,1] op_sel_hi:[0,0] neg_lo:[1,1] neg_hi:[1,0]
	v_pk_fma_f32 v[20:21], v[50:51], v[20:21], v[28:29] op_sel_hi:[0,1,1]
	v_pk_add_f32 v[28:29], v[22:23], v[30:31]
	v_pk_add_f32 v[22:23], v[22:23], v[30:31] neg_lo:[0,1] neg_hi:[0,1]
	s_nop 0
	v_xor_b32_e32 v31, 0x80000000, v22
	v_mov_b32_e32 v30, v23
	v_pk_add_f32 v[22:23], v[24:25], v[32:33]
	v_pk_add_f32 v[24:25], v[24:25], v[32:33] neg_lo:[0,1] neg_hi:[0,1]
	s_nop 0
	v_pk_mul_f32 v[32:33], v[50:51], v[24:25] op_sel:[0,1] op_sel_hi:[0,0] neg_lo:[1,1] neg_hi:[1,0]
	v_pk_fma_f32 v[24:25], v[50:51], v[24:25], v[32:33] op_sel_hi:[0,1,1] neg_lo:[1,0,0] neg_hi:[1,0,0]
	v_pk_add_f32 v[32:33], v[40:41], v[28:29]
	v_pk_add_f32 v[28:29], v[40:41], v[28:29] neg_lo:[0,1] neg_hi:[0,1]
	v_pk_add_f32 v[40:41], v[42:43], v[22:23]
	v_pk_add_f32 v[22:23], v[42:43], v[22:23] neg_lo:[0,1] neg_hi:[0,1]
	s_nop 0
	v_xor_b32_e32 v43, 0x80000000, v22
	v_mov_b32_e32 v42, v23
	v_pk_add_f32 v[22:23], v[32:33], v[40:41]
	v_pk_add_f32 v[32:33], v[32:33], v[40:41] neg_lo:[0,1] neg_hi:[0,1]
	v_pk_add_f32 v[40:41], v[28:29], v[42:43]
	v_pk_add_f32 v[28:29], v[28:29], v[42:43] neg_lo:[0,1] neg_hi:[0,1]
	v_pk_add_f32 v[42:43], v[18:19], v[30:31]
	v_pk_add_f32 v[18:19], v[18:19], v[30:31] neg_lo:[0,1] neg_hi:[0,1]
	v_pk_add_f32 v[30:31], v[20:21], v[24:25]
	v_pk_add_f32 v[20:21], v[20:21], v[24:25] neg_lo:[0,1] neg_hi:[0,1]
	s_nop 0
	v_xor_b32_e32 v25, 0x80000000, v20
	v_mov_b32_e32 v24, v21
	v_pk_add_f32 v[20:21], v[42:43], v[30:31]
	v_pk_add_f32 v[30:31], v[42:43], v[30:31] neg_lo:[0,1] neg_hi:[0,1]
	v_pk_add_f32 v[42:43], v[18:19], v[24:25]
	v_pk_add_f32 v[18:19], v[18:19], v[24:25] neg_lo:[0,1] neg_hi:[0,1]
	v_add_u32_e32 v24, 0x2000, v14
	v_ashrrev_i32_e32 v25, 31, v24
	v_lshl_add_u64 v[24:25], v[24:25], 3, s[48:49]
	global_store_dwordx2 v[24:25], v[36:37], off
	v_add_u32_e32 v24, 0x2200, v14
	v_ashrrev_i32_e32 v25, 31, v24
	v_lshl_add_u64 v[24:25], v[24:25], 3, s[48:49]
	global_store_dwordx2 v[24:25], v[22:23], off
	v_add_u32_e32 v22, 0x2400, v14
	v_ashrrev_i32_e32 v23, 31, v22
	v_lshl_add_u64 v[22:23], v[22:23], 3, s[48:49]
	global_store_dwordx2 v[22:23], v[26:27], off
	v_add_u32_e32 v22, 0x2600, v14
	v_ashrrev_i32_e32 v23, 31, v22
	v_lshl_add_u64 v[22:23], v[22:23], 3, s[48:49]
	global_store_dwordx2 v[22:23], v[20:21], off
	v_add_u32_e32 v20, 0x2800, v14
	v_ashrrev_i32_e32 v21, 31, v20
	v_lshl_add_u64 v[20:21], v[20:21], 3, s[48:49]
	global_store_dwordx2 v[20:21], v[48:49], off
	v_add_u32_e32 v20, 0x2a00, v14
	v_ashrrev_i32_e32 v21, 31, v20
	v_lshl_add_u64 v[20:21], v[20:21], 3, s[48:49]
	global_store_dwordx2 v[20:21], v[40:41], off
	v_add_u32_e32 v20, 0x2c00, v14
	v_ashrrev_i32_e32 v21, 31, v20
	v_lshl_add_u64 v[20:21], v[20:21], 3, s[48:49]
	global_store_dwordx2 v[20:21], v[52:53], off
	v_add_u32_e32 v20, 0x2e00, v14
	v_ashrrev_i32_e32 v21, 31, v20
	v_lshl_add_u64 v[20:21], v[20:21], 3, s[48:49]
	global_store_dwordx2 v[20:21], v[42:43], off
	v_add_u32_e32 v20, 0x3000, v14
	v_ashrrev_i32_e32 v21, 31, v20
	v_lshl_add_u64 v[20:21], v[20:21], 3, s[48:49]
	global_store_dwordx2 v[20:21], v[46:47], off
	v_add_u32_e32 v20, 0x3200, v14
	v_ashrrev_i32_e32 v21, 31, v20
	v_lshl_add_u64 v[20:21], v[20:21], 3, s[48:49]
	global_store_dwordx2 v[20:21], v[32:33], off
	v_add_u32_e32 v20, 0x3400, v14
	v_ashrrev_i32_e32 v21, 31, v20
	v_lshl_add_u64 v[20:21], v[20:21], 3, s[48:49]
	global_store_dwordx2 v[20:21], v[44:45], off
	v_add_u32_e32 v20, 0x3600, v14
	v_ashrrev_i32_e32 v21, 31, v20
	v_lshl_add_u64 v[20:21], v[20:21], 3, s[48:49]
	global_store_dwordx2 v[20:21], v[30:31], off
	v_add_u32_e32 v20, 0x3800, v14
	v_ashrrev_i32_e32 v21, 31, v20
	v_lshl_add_u64 v[20:21], v[20:21], 3, s[48:49]
	global_store_dwordx2 v[20:21], v[34:35], off
	v_add_u32_e32 v20, 0x3a00, v14
	v_ashrrev_i32_e32 v21, 31, v20
	v_lshl_add_u64 v[20:21], v[20:21], 3, s[48:49]
	global_store_dwordx2 v[20:21], v[28:29], off
	v_add_u32_e32 v20, 0x3c00, v14
	v_add_u32_e32 v14, 0x3e00, v14
	v_ashrrev_i32_e32 v15, 31, v14
	v_ashrrev_i32_e32 v21, 31, v20
	v_lshl_add_u64 v[14:15], v[14:15], 3, s[48:49]
	v_lshl_add_u64 v[20:21], v[20:21], 3, s[48:49]
	global_store_dwordx2 v[14:15], v[18:19], off
	v_mov_b32_e32 v14, v1
	global_store_dwordx2 v[20:21], v[38:39], off
	s_barrier
	v_mov_b32_e32 v40, v170
	v_ashrrev_i32_e32 v15, 31, v14
	v_lshl_add_u64 v[18:19], v[14:15], 2, s[66:67]
	v_add_co_u32_e32 v28, vcc, s85, v18
	global_load_dword v20, v[18:19], off
	global_load_dword v21, v[18:19], off offset:2048
	v_addc_co_u32_e32 v29, vcc, 0, v19, vcc
	v_add_co_u32_e32 v22, vcc, s84, v18
	v_mov_b32_e32 v15, v174
	s_nop 0
	v_addc_co_u32_e32 v23, vcc, 0, v19, vcc
	v_add_co_u32_e32 v30, vcc, s61, v18
	v_mov_b32_e32 v45, v11
	s_nop 0
	v_addc_co_u32_e32 v31, vcc, 0, v19, vcc
	v_add_co_u32_e32 v32, vcc, s45, v18
	s_nop 1
	v_addc_co_u32_e32 v33, vcc, 0, v19, vcc
	v_add_co_u32_e32 v34, vcc, s88, v18
	global_load_dword v26, v[22:23], off offset:-4096
	global_load_dword v24, v[22:23], off
	global_load_dword v25, v[22:23], off offset:2048
	s_nop 0
	global_load_dword v22, v[32:33], off offset:-4096
	v_addc_co_u32_e32 v35, vcc, 0, v19, vcc
	v_add_co_u32_e32 v36, vcc, s0, v18
	s_mov_b32 s0, 0xa000
	s_nop 0
	v_addc_co_u32_e32 v37, vcc, 0, v19, vcc
	v_add_co_u32_e32 v38, vcc, s0, v18
	s_mov_b32 s0, 0x9000
	s_nop 0
	v_addc_co_u32_e32 v39, vcc, 0, v19, vcc
	global_load_dword v43, v[32:33], off offset:2048
	global_load_dword v46, v[34:35], off offset:-4096
	global_load_dword v48, v[36:37], off
	global_load_dword v49, v[36:37], off offset:2048
	global_load_dword v62, v[34:35], off
	global_load_dword v63, v[34:35], off offset:2048
	s_nop 0
	global_load_dword v34, v[38:39], off offset:-4096
	global_load_dword v64, v[36:37], off offset:-4096
	v_add_co_u32_e32 v36, vcc, s0, v18
	s_mov_b32 s0, 0xb000
	s_nop 0
	v_addc_co_u32_e32 v37, vcc, 0, v19, vcc
	global_load_dword v27, v[28:29], off offset:2048
	global_load_dword v35, v[36:37], off offset:2048
	v_add_co_u32_e32 v28, vcc, s86, v18
	global_load_dword v66, v[38:39], off
	global_load_dword v67, v[38:39], off offset:2048
	v_addc_co_u32_e32 v29, vcc, 0, v19, vcc
	v_add_co_u32_e32 v36, vcc, s0, v18
	s_mov_b32 s0, 0xc000
	s_nop 0
	v_addc_co_u32_e32 v37, vcc, 0, v19, vcc
	v_add_co_u32_e32 v38, vcc, s0, v18
	s_mov_b32 s0, 0xe000
	s_nop 0
	v_addc_co_u32_e32 v39, vcc, 0, v19, vcc
	global_load_dword v68, v[38:39], off offset:-4096
	global_load_dword v23, v[30:31], off offset:2048
	global_load_dword v69, v[36:37], off offset:2048
	v_add_co_u32_e32 v30, vcc, s90, v18
	s_waitcnt vmcnt(11)
	v_sub_f32_e32 v44, v21, v49
	v_addc_co_u32_e32 v31, vcc, 0, v19, vcc
	global_load_dword v47, v[28:29], off offset:2048
	global_load_dword v65, v[30:31], off offset:2048
	global_load_dword v42, v[32:33], off
	s_nop 0
	global_load_dword v30, v[38:39], off
	global_load_dword v31, v[38:39], off offset:2048
	v_add_co_u32_e32 v28, vcc, s0, v18
	s_mov_b32 s0, 0xd000
	s_nop 0
	v_addc_co_u32_e32 v29, vcc, 0, v19, vcc
	global_load_dword v32, v[28:29], off offset:-4096
	v_add_co_u32_e32 v36, vcc, s0, v18
	s_mov_b32 s0, 0xf000
	s_nop 0
	v_addc_co_u32_e32 v37, vcc, 0, v19, vcc
	global_load_dword v33, v[36:37], off offset:2048
	global_load_dword v38, v[28:29], off
	global_load_dword v39, v[28:29], off offset:2048
	v_add_co_u32_e32 v18, vcc, s0, v18
	v_mov_b32_e32 v36, v166
	s_nop 0
	v_addc_co_u32_e32 v19, vcc, 0, v19, vcc
	global_load_dword v70, v[18:19], off
	global_load_dword v71, v[18:19], off offset:2048
	v_mov_b32_e32 v28, v168
	v_mov_b32_e32 v13, v44
	s_nop 0
	v_pk_mul_f32 v[50:51], v[12:13], v[78:79] op_sel_hi:[1,0] neg_lo:[0,1] neg_hi:[0,1]
	s_waitcnt vmcnt(6)
	v_sub_f32_e32 v82, v43, v31
	v_pk_fma_f32 v[44:45], v[44:45], v[72:73], v[50:51] op_sel_hi:[1,0,1]
	v_sub_f32_e32 v50, v26, v34
	v_mov_b32_e32 v13, v50
	v_mov_b32_e32 v51, v11
	v_pk_mul_f32 v[52:53], v[12:13], v[40:41] op_sel_hi:[1,0] neg_lo:[0,1] neg_hi:[0,1]
	v_pk_mul_f32 v[84:85], v[82:83], v[78:79] op_sel_hi:[1,0] neg_lo:[0,1] neg_hi:[0,1]
	v_pk_fma_f32 v[50:51], v[50:51], v[36:37], v[52:53] op_sel_hi:[1,0,1]
	v_sub_f32_e32 v52, v27, v35
	v_mov_b32_e32 v13, v52
	v_mov_b32_e32 v53, v11
	v_pk_mul_f32 v[54:55], v[12:13], v[76:77] op_sel_hi:[1,0] neg_lo:[0,1] neg_hi:[0,1]
	v_sub_f32_e32 v10, v20, v48
	v_pk_fma_f32 v[54:55], v[52:53], v[74:75], v[54:55] op_sel_hi:[1,0,1]
	v_sub_f32_e32 v52, v24, v66
	v_mov_b32_e32 v13, v52
	v_pk_mul_f32 v[56:57], v[12:13], v[28:29] op_sel_hi:[1,0] neg_lo:[0,1] neg_hi:[0,1]
	v_pk_add_f32 v[20:21], v[20:21], v[48:49]
	v_pk_fma_f32 v[56:57], v[52:53], v[28:29], v[56:57] op_sel_hi:[1,0,1]
	v_sub_f32_e32 v52, v25, v67
	v_pk_mul_f32 v[58:59], v[52:53], v[76:77] op_sel_hi:[1,0]
	v_mov_b32_e32 v13, v52
	v_sub_f32_e32 v52, v22, v68
	v_pk_fma_f32 v[60:61], v[12:13], v[74:75], v[58:59] op_sel_hi:[1,0,1] neg_lo:[0,1,0] neg_hi:[0,1,0]
	v_pk_mul_f32 v[58:59], v[52:53], v[40:41] op_sel_hi:[1,0]
	v_mov_b32_e32 v13, v52
	v_sub_f32_e32 v52, v23, v69
	v_pk_fma_f32 v[58:59], v[12:13], v[36:37], v[58:59] op_sel_hi:[1,0,1] neg_lo:[0,1,0] neg_hi:[0,1,0]
	v_pk_mul_f32 v[80:81], v[52:53], v[78:79] op_sel_hi:[1,0]
	v_mov_b32_e32 v13, v52
	v_pk_fma_f32 v[52:53], v[12:13], v[72:73], v[80:81] op_sel_hi:[1,0,1] neg_lo:[0,1,0] neg_hi:[0,1,0]
	v_sub_f32_e32 v13, v42, v30
	v_xor_b32_e32 v81, 0x80000000, v13
	v_mov_b32_e32 v13, v82
	v_pk_fma_f32 v[82:83], v[12:13], v[72:73], v[84:85] op_sel_hi:[1,0,1] neg_lo:[0,1,0] neg_hi:[0,1,0]
	s_waitcnt vmcnt(5)
	v_sub_f32_e32 v84, v46, v32
	v_mov_b32_e32 v85, v11
	v_pk_mul_f32 v[86:87], v[84:85], v[40:41] op_sel_hi:[1,0] neg_lo:[0,1] neg_hi:[0,1]
	v_mov_b32_e32 v13, v84
	v_pk_fma_f32 v[84:85], v[12:13], v[36:37], v[86:87] op_sel_hi:[1,0,1] neg_lo:[0,1,0] neg_hi:[0,1,0]
	s_waitcnt vmcnt(4)
	v_sub_f32_e32 v86, v47, v33
	v_mov_b32_e32 v87, v11
	v_pk_mul_f32 v[88:89], v[86:87], v[76:77] op_sel_hi:[1,0] neg_lo:[0,1] neg_hi:[0,1]
	v_mov_b32_e32 v13, v86
	v_pk_fma_f32 v[86:87], v[12:13], v[74:75], v[88:89] op_sel_hi:[1,0,1] neg_lo:[0,1,0] neg_hi:[0,1,0]
	s_waitcnt vmcnt(3)
	v_sub_f32_e32 v88, v62, v38
	v_mov_b32_e32 v13, v88
	v_mov_b32_e32 v89, v11
	v_pk_mul_f32 v[90:91], v[12:13], v[28:29] op_sel_hi:[1,0] neg_lo:[0,1] neg_hi:[0,1]
	v_pk_add_f32 v[30:31], v[42:43], v[30:31]
	v_pk_fma_f32 v[88:89], v[88:89], v[28:29], v[90:91] op_sel_hi:[1,0,1] neg_lo:[0,1,0] neg_hi:[0,1,0]
	s_waitcnt vmcnt(2)
	v_sub_f32_e32 v90, v63, v39
	v_mov_b32_e32 v13, v90
	v_mov_b32_e32 v91, v11
	v_pk_mul_f32 v[76:77], v[12:13], v[76:77] op_sel_hi:[1,0] neg_lo:[0,1] neg_hi:[0,1]
	v_pk_add_f32 v[42:43], v[20:21], v[30:31] neg_lo:[0,1] neg_hi:[0,1]
	v_pk_fma_f32 v[74:75], v[90:91], v[74:75], v[76:77] op_sel_hi:[1,0,1] neg_lo:[0,1,0] neg_hi:[0,1,0]
	s_waitcnt vmcnt(1)
	v_sub_f32_e32 v76, v64, v70
	v_mov_b32_e32 v13, v76
	v_mov_b32_e32 v77, v11
	v_pk_mul_f32 v[90:91], v[12:13], v[40:41] op_sel_hi:[1,0] neg_lo:[0,1] neg_hi:[0,1]
	v_pk_add_f32 v[26:27], v[26:27], v[34:35]
	v_pk_fma_f32 v[76:77], v[76:77], v[36:37], v[90:91] op_sel_hi:[1,0,1] neg_lo:[0,1,0] neg_hi:[0,1,0]
	s_waitcnt vmcnt(0)
	v_sub_f32_e32 v90, v65, v71
	v_mov_b32_e32 v13, v90
	v_pk_mul_f32 v[78:79], v[12:13], v[78:79] op_sel_hi:[1,0] neg_lo:[0,1] neg_hi:[0,1]
	v_mov_b32_e32 v13, v43
	v_pk_add_f32 v[32:33], v[46:47], v[32:33]
	v_mov_b32_e32 v46, v42
	v_pk_add_f32 v[20:21], v[20:21], v[30:31]
	v_mov_b32_e32 v30, v43
	v_mov_b32_e32 v31, v11
	v_pk_mul_f32 v[42:43], v[12:13], v[40:41] op_sel_hi:[1,0] neg_lo:[0,1] neg_hi:[0,1]
	v_pk_add_f32 v[34:35], v[62:63], v[38:39]
	v_pk_fma_f32 v[62:63], v[30:31], v[36:37], v[42:43] op_sel_hi:[1,0,1]
	v_pk_add_f32 v[30:31], v[26:27], v[32:33] neg_lo:[0,1] neg_hi:[0,1]
	v_pk_add_f32 v[24:25], v[24:25], v[66:67]
	v_mov_b32_e32 v13, v30
	v_mov_b32_e32 v42, v30
	v_pk_mul_f32 v[48:49], v[12:13], v[28:29] op_sel_hi:[1,0] neg_lo:[0,1] neg_hi:[0,1]
	v_pk_add_f32 v[26:27], v[26:27], v[32:33]
	v_mov_b32_e32 v32, v31
	v_mov_b32_e32 v33, v11
	v_mov_b32_e32 v13, v31
	v_pk_add_f32 v[30:31], v[24:25], v[34:35] neg_lo:[0,1] neg_hi:[0,1]
	v_pk_add_f32 v[22:23], v[22:23], v[68:69]
	v_pk_add_f32 v[38:39], v[64:65], v[70:71]
	v_pk_mul_f32 v[32:33], v[32:33], v[40:41] op_sel_hi:[1,0]
	v_pk_add_f32 v[24:25], v[24:25], v[34:35]
	v_mov_b32_e32 v34, v31
	v_mov_b32_e32 v35, v11
	v_pk_fma_f32 v[32:33], v[12:13], v[36:37], v[32:33] op_sel_hi:[1,0,1] neg_lo:[0,1,0] neg_hi:[0,1,0]
	v_xor_b32_e32 v67, 0x80000000, v30
	v_pk_mul_f32 v[34:35], v[34:35], v[40:41] op_sel_hi:[1,0] neg_lo:[0,1] neg_hi:[0,1]
	v_mov_b32_e32 v13, v31
	v_pk_add_f32 v[30:31], v[22:23], v[38:39] neg_lo:[0,1] neg_hi:[0,1]
	v_mov_b32_e32 v43, v11
	v_pk_fma_f32 v[68:69], v[12:13], v[36:37], v[34:35] op_sel_hi:[1,0,1] neg_lo:[0,1,0] neg_hi:[0,1,0]
	v_mov_b32_e32 v13, v30
	v_pk_fma_f32 v[64:65], v[42:43], v[28:29], v[48:49] op_sel_hi:[1,0,1]
	v_mov_b32_e32 v34, v30
	v_mov_b32_e32 v35, v11
	v_pk_mul_f32 v[42:43], v[12:13], v[28:29] op_sel_hi:[1,0] neg_lo:[0,1] neg_hi:[0,1]
	v_mov_b32_e32 v13, v31
	v_pk_fma_f32 v[70:71], v[34:35], v[28:29], v[42:43] op_sel_hi:[1,0,1] neg_lo:[0,1,0] neg_hi:[0,1,0]
	v_mov_b32_e32 v34, v31
	v_pk_mul_f32 v[30:31], v[12:13], v[40:41] op_sel_hi:[1,0] neg_lo:[0,1] neg_hi:[0,1]
	v_pk_add_f32 v[22:23], v[22:23], v[38:39]
	v_pk_fma_f32 v[38:39], v[34:35], v[36:37], v[30:31] op_sel_hi:[1,0,1] neg_lo:[0,1,0] neg_hi:[0,1,0]
	v_pk_add_f32 v[30:31], v[20:21], v[24:25] neg_lo:[0,1] neg_hi:[0,1]
	v_pk_add_f32 v[20:21], v[20:21], v[24:25]
	v_mov_b32_e32 v13, v31
	v_mov_b32_e32 v42, v30
	v_mov_b32_e32 v24, v31
	v_mov_b32_e32 v25, v11
	v_pk_mul_f32 v[30:31], v[12:13], v[28:29] op_sel_hi:[1,0] neg_lo:[0,1] neg_hi:[0,1]
	v_mov_b32_e32 v91, v11
	v_pk_fma_f32 v[30:31], v[24:25], v[28:29], v[30:31] op_sel_hi:[1,0,1]
	v_pk_add_f32 v[24:25], v[26:27], v[22:23] neg_lo:[0,1] neg_hi:[0,1]
	v_pk_fma_f32 v[72:73], v[90:91], v[72:73], v[78:79] op_sel_hi:[1,0,1] neg_lo:[0,1,0] neg_hi:[0,1,0]
	v_mov_b32_e32 v13, v25
	v_xor_b32_e32 v79, 0x80000000, v24
	v_pk_add_f32 v[22:23], v[26:27], v[22:23]
	v_mov_b32_e32 v26, v25
	v_mov_b32_e32 v27, v11
	v_pk_mul_f32 v[24:25], v[12:13], v[28:29] op_sel_hi:[1,0] neg_lo:[0,1] neg_hi:[0,1]
	v_pk_add_f32 v[34:35], v[20:21], v[22:23]
	v_pk_fma_f32 v[26:27], v[26:27], v[28:29], v[24:25] op_sel_hi:[1,0,1] neg_lo:[0,1,0] neg_hi:[0,1,0]
	v_pk_add_f32 v[24:25], v[20:21], v[22:23] neg_lo:[0,1] neg_hi:[0,1]
	v_mov_b32_e32 v43, v11
	v_pk_add_f32 v[20:21], v[24:25], 0 neg_lo:[1,1] neg_hi:[1,1]
	v_mov_b32_e32 v78, v11
	v_mov_b32_e32 v90, v24
	v_mov_b32_e32 v20, v11
	v_pk_add_f32 v[48:49], v[90:91], v[20:21]
	v_pk_add_f32 v[24:25], v[90:91], v[20:21] neg_lo:[0,1] neg_hi:[0,1]
	v_pk_add_f32 v[20:21], v[42:43], v[78:79]
	v_pk_add_f32 v[22:23], v[42:43], v[78:79] neg_lo:[0,1] neg_hi:[0,1]
	v_pk_add_f32 v[42:43], v[30:31], v[26:27]
	v_pk_add_f32 v[26:27], v[30:31], v[26:27] neg_lo:[0,1] neg_hi:[0,1]
	v_mov_b32_e32 v47, v11
	v_mov_b32_e32 v66, v11
	v_xor_b32_e32 v79, 0x80000000, v26
	v_mov_b32_e32 v78, v27
	v_pk_add_f32 v[26:27], v[62:63], v[68:69]
	v_pk_add_f32 v[62:63], v[62:63], v[68:69] neg_lo:[0,1] neg_hi:[0,1]
	v_pk_add_f32 v[90:91], v[20:21], v[42:43]
	v_pk_add_f32 v[30:31], v[20:21], v[42:43] neg_lo:[0,1] neg_hi:[0,1]
	v_pk_add_f32 v[42:43], v[22:23], v[78:79]
	v_pk_add_f32 v[20:21], v[22:23], v[78:79] neg_lo:[0,1] neg_hi:[0,1]
	v_pk_add_f32 v[22:23], v[46:47], v[66:67]
	v_pk_add_f32 v[46:47], v[46:47], v[66:67] neg_lo:[0,1] neg_hi:[0,1]
	v_pk_mul_f32 v[66:67], v[28:29], v[62:63] op_sel:[0,1] op_sel_hi:[0,0] neg_lo:[1,1] neg_hi:[1,0]
	v_pk_fma_f32 v[66:67], v[28:29], v[62:63], v[66:67] op_sel_hi:[0,1,1]
	v_pk_add_f32 v[62:63], v[64:65], v[70:71]
	v_pk_add_f32 v[64:65], v[64:65], v[70:71] neg_lo:[0,1] neg_hi:[0,1]
	v_mov_b32_e32 v80, v11
	v_xor_b32_e32 v69, 0x80000000, v64
	v_mov_b32_e32 v68, v65
	v_pk_add_f32 v[64:65], v[32:33], v[38:39]
	v_pk_add_f32 v[32:33], v[32:33], v[38:39] neg_lo:[0,1] neg_hi:[0,1]
	v_pk_add_f32 v[78:79], v[44:45], v[82:83]
	v_pk_mul_f32 v[38:39], v[28:29], v[32:33] op_sel:[0,1] op_sel_hi:[0,0] neg_lo:[1,1] neg_hi:[1,0]
	v_pk_fma_f32 v[32:33], v[28:29], v[32:33], v[38:39] op_sel_hi:[0,1,1] neg_lo:[1,0,0] neg_hi:[1,0,0]
	v_pk_add_f32 v[38:39], v[22:23], v[62:63]
	v_pk_add_f32 v[22:23], v[22:23], v[62:63] neg_lo:[0,1] neg_hi:[0,1]
	v_pk_add_f32 v[62:63], v[26:27], v[64:65]
	v_pk_add_f32 v[26:27], v[26:27], v[64:65] neg_lo:[0,1] neg_hi:[0,1]
	v_pk_add_f32 v[70:71], v[38:39], v[62:63]
	v_pk_add_f32 v[38:39], v[38:39], v[62:63] neg_lo:[0,1] neg_hi:[0,1]
	v_pk_add_f32 v[62:63], v[22:23], v[26:27] op_sel:[0,1] op_sel_hi:[1,0] neg_hi:[0,1]
	v_pk_add_f32 v[26:27], v[22:23], v[26:27] op_sel:[0,1] op_sel_hi:[1,0] neg_lo:[0,1]
	v_pk_add_f32 v[22:23], v[46:47], v[68:69]
	v_pk_add_f32 v[64:65], v[46:47], v[68:69] neg_lo:[0,1] neg_hi:[0,1]
	v_pk_add_f32 v[46:47], v[66:67], v[32:33]
	v_pk_add_f32 v[32:33], v[66:67], v[32:33] neg_lo:[0,1] neg_hi:[0,1]
	v_pk_add_f32 v[44:45], v[44:45], v[82:83] neg_lo:[0,1] neg_hi:[0,1]
	v_xor_b32_e32 v67, 0x80000000, v32
	v_mov_b32_e32 v66, v33
	v_pk_add_f32 v[68:69], v[22:23], v[46:47]
	v_pk_add_f32 v[32:33], v[22:23], v[46:47] neg_lo:[0,1] neg_hi:[0,1]
	v_pk_add_f32 v[46:47], v[64:65], v[66:67]
	v_pk_add_f32 v[22:23], v[64:65], v[66:67] neg_lo:[0,1] neg_hi:[0,1]
	v_pk_add_f32 v[64:65], v[10:11], v[80:81]
	v_pk_add_f32 v[66:67], v[10:11], v[80:81] neg_lo:[0,1] neg_hi:[0,1]
	v_pk_mul_f32 v[80:81], v[40:41], v[44:45] op_sel:[0,1] op_sel_hi:[0,0] neg_lo:[1,1] neg_hi:[1,0]
	v_pk_fma_f32 v[44:45], v[36:37], v[44:45], v[80:81] op_sel_hi:[0,1,1]
	v_pk_add_f32 v[80:81], v[50:51], v[84:85]
	v_pk_add_f32 v[50:51], v[50:51], v[84:85] neg_lo:[0,1] neg_hi:[0,1]
	v_add_f32_e32 v10, v34, v35
	v_pk_mul_f32 v[82:83], v[28:29], v[50:51] op_sel:[0,1] op_sel_hi:[0,0] neg_lo:[1,1] neg_hi:[1,0]
	v_pk_fma_f32 v[82:83], v[28:29], v[50:51], v[82:83] op_sel_hi:[0,1,1]
	v_pk_add_f32 v[50:51], v[54:55], v[86:87]
	v_pk_add_f32 v[54:55], v[54:55], v[86:87] neg_lo:[0,1] neg_hi:[0,1]
	v_pk_fma_f32 v[16:17], v[10:11], s[42:43], v[16:17] op_sel_hi:[0,1,1]
	v_pk_mul_f32 v[84:85], v[36:37], v[54:55] op_sel:[0,1] op_sel_hi:[0,0] neg_lo:[1,1] neg_hi:[1,0]
	v_pk_fma_f32 v[84:85], v[40:41], v[54:55], v[84:85] op_sel_hi:[0,1,1]
	v_pk_add_f32 v[54:55], v[56:57], v[88:89]
	v_pk_add_f32 v[56:57], v[56:57], v[88:89] neg_lo:[0,1] neg_hi:[0,1]
	v_lshl_add_u32 v13, v15, 3, 0
	v_xor_b32_e32 v87, 0x80000000, v56
	v_mov_b32_e32 v86, v57
	v_pk_add_f32 v[56:57], v[60:61], v[74:75]
	v_pk_add_f32 v[60:61], v[60:61], v[74:75] neg_lo:[0,1] neg_hi:[0,1]
	ds_write_b64 v13, v[16:17]
	v_pk_mul_f32 v[74:75], v[36:37], v[60:61] op_sel:[0,1] op_sel_hi:[0,0] neg_lo:[1,1] neg_hi:[1,0]
	v_pk_fma_f32 v[60:61], v[40:41], v[60:61], v[74:75] op_sel_hi:[0,1,1] neg_lo:[1,0,0] neg_hi:[1,0,0]
	v_pk_add_f32 v[74:75], v[58:59], v[76:77]
	v_pk_add_f32 v[58:59], v[58:59], v[76:77] neg_lo:[0,1] neg_hi:[0,1]
	v_pk_fma_f32 v[16:17], v[180:181], s[92:93], v[180:181] op_sel:[1,0,0] op_sel_hi:[0,1,1]
	v_pk_mul_f32 v[76:77], v[28:29], v[58:59] op_sel:[0,1] op_sel_hi:[0,0] neg_lo:[1,1] neg_hi:[1,0]
	v_pk_fma_f32 v[58:59], v[28:29], v[58:59], v[76:77] op_sel_hi:[0,1,1] neg_lo:[1,0,0] neg_hi:[1,0,0]
	v_pk_add_f32 v[76:77], v[52:53], v[72:73]
	v_pk_add_f32 v[52:53], v[52:53], v[72:73] neg_lo:[0,1] neg_hi:[0,1]
	s_nop 0
	v_pk_mul_f32 v[40:41], v[40:41], v[52:53] op_sel:[0,1] op_sel_hi:[0,0] neg_lo:[1,1] neg_hi:[1,0]
	v_pk_fma_f32 v[52:53], v[36:37], v[52:53], v[40:41] op_sel_hi:[0,1,1] neg_lo:[1,0,0] neg_hi:[1,0,0]
	v_pk_add_f32 v[36:37], v[64:65], v[54:55]
	v_pk_add_f32 v[64:65], v[64:65], v[54:55] neg_lo:[0,1] neg_hi:[0,1]
	v_pk_add_f32 v[54:55], v[78:79], v[56:57] neg_lo:[0,1] neg_hi:[0,1]
	v_pk_add_f32 v[40:41], v[56:57], v[78:79]
	v_pk_mul_f32 v[56:57], v[28:29], v[54:55] op_sel:[0,1] op_sel_hi:[0,0] neg_lo:[1,1] neg_hi:[1,0]
	v_pk_add_f32 v[72:73], v[80:81], v[74:75] neg_lo:[0,1] neg_hi:[0,1]
	v_pk_fma_f32 v[56:57], v[28:29], v[54:55], v[56:57] op_sel_hi:[0,1,1]
	v_pk_add_f32 v[54:55], v[80:81], v[74:75]
	v_xor_b32_e32 v75, 0x80000000, v72
	v_mov_b32_e32 v74, v73
	v_pk_add_f32 v[72:73], v[50:51], v[76:77]
	v_pk_add_f32 v[50:51], v[50:51], v[76:77] neg_lo:[0,1] neg_hi:[0,1]
	s_nop 0
	v_pk_mul_f32 v[76:77], v[28:29], v[50:51] op_sel:[0,1] op_sel_hi:[0,0] neg_lo:[1,1] neg_hi:[1,0]
	v_pk_fma_f32 v[50:51], v[28:29], v[50:51], v[76:77] op_sel_hi:[0,1,1] neg_lo:[1,0,0] neg_hi:[1,0,0]
	v_pk_add_f32 v[76:77], v[36:37], v[54:55]
	v_pk_add_f32 v[36:37], v[36:37], v[54:55] neg_lo:[0,1] neg_hi:[0,1]
	v_pk_add_f32 v[54:55], v[40:41], v[72:73]
	v_pk_add_f32 v[40:41], v[40:41], v[72:73] neg_lo:[0,1] neg_hi:[0,1]
	v_pk_add_f32 v[78:79], v[76:77], v[54:55]
	v_pk_add_f32 v[54:55], v[76:77], v[54:55] neg_lo:[0,1] neg_hi:[0,1]
	v_pk_add_f32 v[76:77], v[36:37], v[40:41] op_sel:[0,1] op_sel_hi:[1,0] neg_hi:[0,1]
	v_pk_add_f32 v[40:41], v[36:37], v[40:41] op_sel:[0,1] op_sel_hi:[1,0] neg_lo:[0,1]
	v_pk_add_f32 v[72:73], v[56:57], v[50:51]
	v_pk_add_f32 v[50:51], v[56:57], v[50:51] neg_lo:[0,1] neg_hi:[0,1]
	v_pk_add_f32 v[36:37], v[64:65], v[74:75]
	v_pk_add_f32 v[64:65], v[64:65], v[74:75] neg_lo:[0,1] neg_hi:[0,1]
	v_xor_b32_e32 v57, 0x80000000, v50
	v_mov_b32_e32 v56, v51
	v_pk_add_f32 v[74:75], v[36:37], v[72:73]
	v_pk_add_f32 v[50:51], v[36:37], v[72:73] neg_lo:[0,1] neg_hi:[0,1]
	v_pk_add_f32 v[72:73], v[64:65], v[56:57]
	v_pk_add_f32 v[36:37], v[64:65], v[56:57] neg_lo:[0,1] neg_hi:[0,1]
	v_pk_add_f32 v[56:57], v[66:67], v[86:87]
	v_pk_add_f32 v[64:65], v[66:67], v[86:87] neg_lo:[0,1] neg_hi:[0,1]
	v_pk_add_f32 v[66:67], v[60:61], v[44:45]
	v_pk_add_f32 v[44:45], v[44:45], v[60:61] neg_lo:[0,1] neg_hi:[0,1]
	s_nop 0
	v_pk_mul_f32 v[60:61], v[28:29], v[44:45] op_sel:[0,1] op_sel_hi:[0,0] neg_lo:[1,1] neg_hi:[1,0]
	v_pk_fma_f32 v[60:61], v[28:29], v[44:45], v[60:61] op_sel_hi:[0,1,1]
	v_pk_add_f32 v[44:45], v[82:83], v[58:59]
	v_pk_add_f32 v[58:59], v[82:83], v[58:59] neg_lo:[0,1] neg_hi:[0,1]
	s_nop 0
	v_xor_b32_e32 v81, 0x80000000, v58
	v_mov_b32_e32 v80, v59
	v_pk_add_f32 v[58:59], v[84:85], v[52:53]
	v_pk_add_f32 v[52:53], v[84:85], v[52:53] neg_lo:[0,1] neg_hi:[0,1]
	s_nop 0
	v_pk_mul_f32 v[82:83], v[28:29], v[52:53] op_sel:[0,1] op_sel_hi:[0,0] neg_lo:[1,1] neg_hi:[1,0]
	v_pk_fma_f32 v[28:29], v[28:29], v[52:53], v[82:83] op_sel_hi:[0,1,1] neg_lo:[1,0,0] neg_hi:[1,0,0]
	v_pk_add_f32 v[52:53], v[56:57], v[44:45]
	v_pk_add_f32 v[44:45], v[56:57], v[44:45] neg_lo:[0,1] neg_hi:[0,1]
	v_pk_add_f32 v[56:57], v[66:67], v[58:59]
	v_pk_add_f32 v[58:59], v[66:67], v[58:59] neg_lo:[0,1] neg_hi:[0,1]
	s_nop 0
	v_pk_add_f32 v[82:83], v[44:45], v[58:59] op_sel:[0,1] op_sel_hi:[1,0] neg_hi:[0,1]
	v_pk_add_f32 v[44:45], v[44:45], v[58:59] op_sel:[0,1] op_sel_hi:[1,0] neg_lo:[0,1]
	v_pk_add_f32 v[66:67], v[60:61], v[28:29]
	v_pk_add_f32 v[28:29], v[60:61], v[28:29] neg_lo:[0,1] neg_hi:[0,1]
	v_pk_add_f32 v[58:59], v[52:53], v[56:57]
	v_pk_add_f32 v[56:57], v[52:53], v[56:57] neg_lo:[0,1] neg_hi:[0,1]
	v_pk_add_f32 v[52:53], v[64:65], v[80:81]
	v_pk_add_f32 v[64:65], v[64:65], v[80:81] neg_lo:[0,1] neg_hi:[0,1]
	v_pk_add_f32 v[80:81], v[52:53], v[66:67]
	v_pk_add_f32 v[52:53], v[52:53], v[66:67] neg_lo:[0,1] neg_hi:[0,1]
	v_pk_add_f32 v[66:67], v[64:65], v[28:29] op_sel:[0,1] op_sel_hi:[1,0] neg_hi:[0,1]
	v_pk_add_f32 v[28:29], v[64:65], v[28:29] op_sel:[0,1] op_sel_hi:[1,0] neg_lo:[0,1]
	v_pk_mul_f32 v[60:61], v[16:17], v[78:79] op_sel:[1,1] op_sel_hi:[0,1] neg_lo:[0,1]
	v_pk_fma_f32 v[60:61], v[16:17], v[78:79], v[60:61] op_sel_hi:[1,0,1]
	ds_write_b64 v13, v[60:61] offset:4224
	v_pk_mul_f32 v[60:61], v[180:181], v[16:17] op_sel:[1,1] op_sel_hi:[0,1] neg_lo:[0,1]
	v_pk_fma_f32 v[16:17], v[180:181], v[16:17], v[60:61] op_sel_hi:[1,0,1]
	s_nop 0
	v_pk_mul_f32 v[60:61], v[16:17], v[70:71] op_sel:[1,1] op_sel_hi:[0,1] neg_lo:[0,1]
	v_pk_fma_f32 v[60:61], v[16:17], v[70:71], v[60:61] op_sel_hi:[1,0,1]
	ds_write_b64 v13, v[60:61] offset:8448
	v_pk_mul_f32 v[60:61], v[180:181], v[16:17] op_sel:[1,1] op_sel_hi:[0,1] neg_lo:[0,1]
	v_pk_fma_f32 v[16:17], v[180:181], v[16:17], v[60:61] op_sel_hi:[1,0,1]
	s_nop 0
	v_pk_mul_f32 v[60:61], v[16:17], v[58:59] op_sel:[1,1] op_sel_hi:[0,1] neg_lo:[0,1]
	v_pk_fma_f32 v[58:59], v[16:17], v[58:59], v[60:61] op_sel_hi:[1,0,1]
	ds_write_b64 v13, v[58:59] offset:12672
	v_pk_mul_f32 v[58:59], v[180:181], v[16:17] op_sel:[1,1] op_sel_hi:[0,1] neg_lo:[0,1]
	v_pk_fma_f32 v[16:17], v[180:181], v[16:17], v[58:59] op_sel_hi:[1,0,1]
	s_nop 0
	v_pk_mul_f32 v[58:59], v[90:91], v[16:17] op_sel:[1,1] op_sel_hi:[1,0] neg_lo:[1,0]
	s_nop 0
	v_pk_fma_f32 v[58:59], v[90:91], v[16:17], v[58:59] op_sel_hi:[0,1,1]
	ds_write_b64 v13, v[58:59] offset:16896
	v_pk_mul_f32 v[58:59], v[180:181], v[16:17] op_sel:[1,1] op_sel_hi:[0,1] neg_lo:[0,1]
	v_pk_fma_f32 v[16:17], v[180:181], v[16:17], v[58:59] op_sel_hi:[1,0,1]
	s_nop 0
	v_pk_mul_f32 v[58:59], v[16:17], v[74:75] op_sel:[1,1] op_sel_hi:[0,1] neg_lo:[0,1]
	v_pk_fma_f32 v[58:59], v[16:17], v[74:75], v[58:59] op_sel_hi:[1,0,1]
	ds_write_b64 v13, v[58:59] offset:21120
	v_pk_mul_f32 v[58:59], v[180:181], v[16:17] op_sel:[1,1] op_sel_hi:[0,1] neg_lo:[0,1]
	v_pk_fma_f32 v[16:17], v[180:181], v[16:17], v[58:59] op_sel_hi:[1,0,1]
	s_nop 0
	v_pk_mul_f32 v[58:59], v[68:69], v[16:17] op_sel:[1,1] op_sel_hi:[1,0] neg_lo:[1,0]
	s_nop 0
	v_pk_fma_f32 v[58:59], v[68:69], v[16:17], v[58:59] op_sel_hi:[0,1,1]
	ds_write_b64 v13, v[58:59] offset:25344
	v_pk_mul_f32 v[58:59], v[180:181], v[16:17] op_sel:[1,1] op_sel_hi:[0,1] neg_lo:[0,1]
	v_pk_fma_f32 v[16:17], v[180:181], v[16:17], v[58:59] op_sel_hi:[1,0,1]
	s_nop 0
	v_pk_mul_f32 v[58:59], v[80:81], v[16:17] op_sel:[1,1] op_sel_hi:[1,0] neg_lo:[1,0]
	s_nop 0
	v_pk_fma_f32 v[58:59], v[80:81], v[16:17], v[58:59] op_sel_hi:[0,1,1]
	ds_write_b64 v13, v[58:59] offset:29568
	v_pk_mul_f32 v[58:59], v[180:181], v[16:17] op_sel:[1,1] op_sel_hi:[0,1] neg_lo:[0,1]
	v_pk_fma_f32 v[16:17], v[180:181], v[16:17], v[58:59] op_sel_hi:[1,0,1]
	s_nop 0
	v_pk_mul_f32 v[58:59], v[48:49], v[16:17] op_sel:[1,1] op_sel_hi:[1,0] neg_lo:[1,0]
	s_nop 0
	v_pk_fma_f32 v[48:49], v[48:49], v[16:17], v[58:59] op_sel_hi:[0,1,1]
	ds_write_b64 v13, v[48:49] offset:33792
	v_pk_mul_f32 v[48:49], v[180:181], v[16:17] op_sel:[1,1] op_sel_hi:[0,1] neg_lo:[0,1]
	v_pk_fma_f32 v[16:17], v[180:181], v[16:17], v[48:49] op_sel_hi:[1,0,1]
	s_nop 0
	v_pk_mul_f32 v[48:49], v[76:77], v[16:17] op_sel:[1,1] op_sel_hi:[1,0] neg_lo:[1,0]
	s_nop 0
	v_pk_fma_f32 v[48:49], v[76:77], v[16:17], v[48:49] op_sel_hi:[0,1,1]
	ds_write_b64 v13, v[48:49] offset:38016
	v_pk_mul_f32 v[48:49], v[180:181], v[16:17] op_sel:[1,1] op_sel_hi:[0,1] neg_lo:[0,1]
	v_pk_fma_f32 v[16:17], v[180:181], v[16:17], v[48:49] op_sel_hi:[1,0,1]
	s_nop 0
	v_pk_mul_f32 v[48:49], v[62:63], v[16:17] op_sel:[1,1] op_sel_hi:[1,0] neg_lo:[1,0]
	s_nop 0
	v_pk_fma_f32 v[48:49], v[62:63], v[16:17], v[48:49] op_sel_hi:[0,1,1]
	ds_write_b64 v13, v[48:49] offset:42240
	v_pk_mul_f32 v[48:49], v[180:181], v[16:17] op_sel:[1,1] op_sel_hi:[0,1] neg_lo:[0,1]
	v_pk_fma_f32 v[16:17], v[180:181], v[16:17], v[48:49] op_sel_hi:[1,0,1]
	s_nop 0
	v_pk_mul_f32 v[48:49], v[82:83], v[16:17] op_sel:[1,1] op_sel_hi:[1,0] neg_lo:[1,0]
	s_nop 0
	v_pk_fma_f32 v[48:49], v[82:83], v[16:17], v[48:49] op_sel_hi:[0,1,1]
	ds_write_b64 v13, v[48:49] offset:46464
	v_pk_mul_f32 v[48:49], v[180:181], v[16:17] op_sel:[1,1] op_sel_hi:[0,1] neg_lo:[0,1]
	v_pk_fma_f32 v[16:17], v[180:181], v[16:17], v[48:49] op_sel_hi:[1,0,1]
	s_nop 0
	v_pk_mul_f32 v[48:49], v[42:43], v[16:17] op_sel:[1,1] op_sel_hi:[1,0] neg_lo:[1,0]
	s_nop 0
	v_pk_fma_f32 v[42:43], v[42:43], v[16:17], v[48:49] op_sel_hi:[0,1,1]
	ds_write_b64 v13, v[42:43] offset:50688
	v_pk_mul_f32 v[42:43], v[180:181], v[16:17] op_sel:[1,1] op_sel_hi:[0,1] neg_lo:[0,1]
	v_pk_fma_f32 v[16:17], v[180:181], v[16:17], v[42:43] op_sel_hi:[1,0,1]
	s_nop 0
	v_pk_mul_f32 v[42:43], v[72:73], v[16:17] op_sel:[1,1] op_sel_hi:[1,0] neg_lo:[1,0]
	s_nop 0
	v_pk_fma_f32 v[42:43], v[72:73], v[16:17], v[42:43] op_sel_hi:[0,1,1]
	ds_write_b64 v13, v[42:43] offset:54912
	v_pk_mul_f32 v[42:43], v[180:181], v[16:17] op_sel:[1,1] op_sel_hi:[0,1] neg_lo:[0,1]
	v_pk_fma_f32 v[16:17], v[180:181], v[16:17], v[42:43] op_sel_hi:[1,0,1]
	s_nop 0
	v_pk_mul_f32 v[42:43], v[46:47], v[16:17] op_sel:[1,1] op_sel_hi:[1,0] neg_lo:[1,0]
	s_nop 0
	v_pk_fma_f32 v[42:43], v[46:47], v[16:17], v[42:43] op_sel_hi:[0,1,1]
	ds_write_b64 v13, v[42:43] offset:59136
	v_pk_mul_f32 v[42:43], v[180:181], v[16:17] op_sel:[1,1] op_sel_hi:[0,1] neg_lo:[0,1]
	v_pk_fma_f32 v[16:17], v[180:181], v[16:17], v[42:43] op_sel_hi:[1,0,1]
	s_nop 0
	v_pk_mul_f32 v[42:43], v[66:67], v[16:17] op_sel:[1,1] op_sel_hi:[1,0] neg_lo:[1,0]
	s_nop 0
	v_pk_fma_f32 v[42:43], v[66:67], v[16:17], v[42:43] op_sel_hi:[0,1,1]
	ds_write_b64 v13, v[42:43] offset:63360
	v_pk_mul_f32 v[42:43], v[180:181], v[16:17] op_sel:[1,1] op_sel_hi:[0,1] neg_lo:[0,1]
	v_pk_fma_f32 v[16:17], v[180:181], v[16:17], v[42:43] op_sel_hi:[1,0,1]
	v_sub_f32_e32 v10, v34, v35
	v_pk_mul_f32 v[34:35], v[16:17], s[46:47]
	s_nop 0
	v_pk_fma_f32 v[34:35], v[10:11], v[16:17], v[34:35] op_sel:[0,0,1] op_sel_hi:[0,1,0]
	v_add_u32_e32 v10, 0x10800, v13
	ds_write_b64 v10, v[34:35]
	v_pk_mul_f32 v[34:35], v[180:181], v[16:17] op_sel:[1,1] op_sel_hi:[0,1] neg_lo:[0,1]
	v_pk_fma_f32 v[16:17], v[180:181], v[16:17], v[34:35] op_sel_hi:[1,0,1]
	s_nop 0
	v_pk_mul_f32 v[34:35], v[54:55], v[16:17] op_sel:[1,1] op_sel_hi:[1,0] neg_lo:[1,0]
	v_add_u32_e32 v10, 0x11880, v13
	v_pk_fma_f32 v[34:35], v[54:55], v[16:17], v[34:35] op_sel_hi:[0,1,1]
	ds_write_b64 v10, v[34:35]
	v_pk_mul_f32 v[34:35], v[180:181], v[16:17] op_sel:[1,1] op_sel_hi:[0,1] neg_lo:[0,1]
	v_pk_fma_f32 v[16:17], v[180:181], v[16:17], v[34:35] op_sel_hi:[1,0,1]
	s_nop 0
	v_pk_mul_f32 v[34:35], v[38:39], v[16:17] op_sel:[1,1] op_sel_hi:[1,0] neg_lo:[1,0]
	v_add_u32_e32 v10, 0x12900, v13
	v_pk_fma_f32 v[34:35], v[38:39], v[16:17], v[34:35] op_sel_hi:[0,1,1]
	ds_write_b64 v10, v[34:35]
	v_pk_mul_f32 v[34:35], v[180:181], v[16:17] op_sel:[1,1] op_sel_hi:[0,1] neg_lo:[0,1]
	v_pk_fma_f32 v[16:17], v[180:181], v[16:17], v[34:35] op_sel_hi:[1,0,1]
	s_nop 0
	v_pk_mul_f32 v[34:35], v[56:57], v[16:17] op_sel:[1,1] op_sel_hi:[1,0] neg_lo:[1,0]
	v_add_u32_e32 v10, 0x13980, v13
	v_pk_fma_f32 v[34:35], v[56:57], v[16:17], v[34:35] op_sel_hi:[0,1,1]
	ds_write_b64 v10, v[34:35]
	v_pk_mul_f32 v[34:35], v[180:181], v[16:17] op_sel:[1,1] op_sel_hi:[0,1] neg_lo:[0,1]
	v_pk_fma_f32 v[16:17], v[180:181], v[16:17], v[34:35] op_sel_hi:[1,0,1]
	s_nop 0
	v_pk_mul_f32 v[34:35], v[30:31], v[16:17] op_sel:[1,1] op_sel_hi:[1,0] neg_lo:[1,0]
	v_add_u32_e32 v10, 0x14a00, v13
	v_pk_fma_f32 v[30:31], v[30:31], v[16:17], v[34:35] op_sel_hi:[0,1,1]
	ds_write_b64 v10, v[30:31]
	v_pk_mul_f32 v[30:31], v[180:181], v[16:17] op_sel:[1,1] op_sel_hi:[0,1] neg_lo:[0,1]
	v_pk_fma_f32 v[16:17], v[180:181], v[16:17], v[30:31] op_sel_hi:[1,0,1]
	s_nop 0
	v_pk_mul_f32 v[30:31], v[50:51], v[16:17] op_sel:[1,1] op_sel_hi:[1,0] neg_lo:[1,0]
	v_add_u32_e32 v10, 0x15a80, v13
	v_pk_fma_f32 v[30:31], v[50:51], v[16:17], v[30:31] op_sel_hi:[0,1,1]
	ds_write_b64 v10, v[30:31]
	v_pk_mul_f32 v[30:31], v[180:181], v[16:17] op_sel:[1,1] op_sel_hi:[0,1] neg_lo:[0,1]
	v_pk_fma_f32 v[16:17], v[180:181], v[16:17], v[30:31] op_sel_hi:[1,0,1]
	s_nop 0
	v_pk_mul_f32 v[30:31], v[32:33], v[16:17] op_sel:[1,1] op_sel_hi:[1,0] neg_lo:[1,0]
	v_add_u32_e32 v10, 0x16b00, v13
	v_pk_fma_f32 v[30:31], v[32:33], v[16:17], v[30:31] op_sel_hi:[0,1,1]
	ds_write_b64 v10, v[30:31]
	v_pk_mul_f32 v[30:31], v[180:181], v[16:17] op_sel:[1,1] op_sel_hi:[0,1] neg_lo:[0,1]
	v_pk_fma_f32 v[16:17], v[180:181], v[16:17], v[30:31] op_sel_hi:[1,0,1]
	s_nop 0
	v_pk_mul_f32 v[30:31], v[52:53], v[16:17] op_sel:[1,1] op_sel_hi:[1,0] neg_lo:[1,0]
	v_add_u32_e32 v10, 0x17b80, v13
	v_pk_fma_f32 v[30:31], v[52:53], v[16:17], v[30:31] op_sel_hi:[0,1,1]
	ds_write_b64 v10, v[30:31]
	v_pk_mul_f32 v[30:31], v[180:181], v[16:17] op_sel:[1,1] op_sel_hi:[0,1] neg_lo:[0,1]
	v_pk_fma_f32 v[16:17], v[180:181], v[16:17], v[30:31] op_sel_hi:[1,0,1]
	s_nop 0
	v_pk_mul_f32 v[30:31], v[24:25], v[16:17] op_sel:[1,1] op_sel_hi:[1,0] neg_lo:[1,0]
	v_add_u32_e32 v10, 0x18c00, v13
	v_pk_fma_f32 v[24:25], v[24:25], v[16:17], v[30:31] op_sel_hi:[0,1,1]
	ds_write_b64 v10, v[24:25]
	v_pk_mul_f32 v[24:25], v[180:181], v[16:17] op_sel:[1,1] op_sel_hi:[0,1] neg_lo:[0,1]
	v_pk_fma_f32 v[16:17], v[180:181], v[16:17], v[24:25] op_sel_hi:[1,0,1]
	s_nop 0
	v_pk_mul_f32 v[24:25], v[40:41], v[16:17] op_sel:[1,1] op_sel_hi:[1,0] neg_lo:[1,0]
	v_add_u32_e32 v10, 0x19c80, v13
	v_pk_fma_f32 v[24:25], v[40:41], v[16:17], v[24:25] op_sel_hi:[0,1,1]
	ds_write_b64 v10, v[24:25]
	v_pk_mul_f32 v[24:25], v[180:181], v[16:17] op_sel:[1,1] op_sel_hi:[0,1] neg_lo:[0,1]
	v_pk_fma_f32 v[16:17], v[180:181], v[16:17], v[24:25] op_sel_hi:[1,0,1]
	s_nop 0
	v_pk_mul_f32 v[24:25], v[26:27], v[16:17] op_sel:[1,1] op_sel_hi:[1,0] neg_lo:[1,0]
	v_add_u32_e32 v10, 0x1ad00, v13
	v_pk_fma_f32 v[24:25], v[26:27], v[16:17], v[24:25] op_sel_hi:[0,1,1]
	ds_write_b64 v10, v[24:25]
	v_pk_mul_f32 v[24:25], v[180:181], v[16:17] op_sel:[1,1] op_sel_hi:[0,1] neg_lo:[0,1]
	v_pk_fma_f32 v[16:17], v[180:181], v[16:17], v[24:25] op_sel_hi:[1,0,1]
	s_nop 0
	v_pk_mul_f32 v[24:25], v[44:45], v[16:17] op_sel:[1,1] op_sel_hi:[1,0] neg_lo:[1,0]
	v_add_u32_e32 v10, 0x1bd80, v13
	v_pk_fma_f32 v[24:25], v[44:45], v[16:17], v[24:25] op_sel_hi:[0,1,1]
	ds_write_b64 v10, v[24:25]
	v_pk_mul_f32 v[24:25], v[180:181], v[16:17] op_sel:[1,1] op_sel_hi:[0,1] neg_lo:[0,1]
	v_pk_fma_f32 v[16:17], v[180:181], v[16:17], v[24:25] op_sel_hi:[1,0,1]
	s_nop 0
	v_pk_mul_f32 v[24:25], v[20:21], v[16:17] op_sel:[1,1] op_sel_hi:[1,0] neg_lo:[1,0]
	v_add_u32_e32 v10, 0x1ce00, v13
	v_pk_fma_f32 v[20:21], v[20:21], v[16:17], v[24:25] op_sel_hi:[0,1,1]
	ds_write_b64 v10, v[20:21]
	v_pk_mul_f32 v[20:21], v[180:181], v[16:17] op_sel:[1,1] op_sel_hi:[0,1] neg_lo:[0,1]
	v_pk_fma_f32 v[16:17], v[180:181], v[16:17], v[20:21] op_sel_hi:[1,0,1]
	s_nop 0
	v_pk_mul_f32 v[20:21], v[36:37], v[16:17] op_sel:[1,1] op_sel_hi:[1,0] neg_lo:[1,0]
	v_add_u32_e32 v10, 0x1de80, v13
	v_pk_fma_f32 v[20:21], v[36:37], v[16:17], v[20:21] op_sel_hi:[0,1,1]
	ds_write_b64 v10, v[20:21]
	v_pk_mul_f32 v[20:21], v[180:181], v[16:17] op_sel:[1,1] op_sel_hi:[0,1] neg_lo:[0,1]
	v_pk_fma_f32 v[16:17], v[180:181], v[16:17], v[20:21] op_sel_hi:[1,0,1]
	s_nop 0
	v_pk_mul_f32 v[20:21], v[22:23], v[16:17] op_sel:[1,1] op_sel_hi:[1,0] neg_lo:[1,0]
	v_add_u32_e32 v10, 0x1ef00, v13
	v_pk_fma_f32 v[20:21], v[22:23], v[16:17], v[20:21] op_sel_hi:[0,1,1]
	ds_write_b64 v10, v[20:21]
	v_pk_mul_f32 v[20:21], v[180:181], v[16:17] op_sel:[1,1] op_sel_hi:[0,1] neg_lo:[0,1]
	v_pk_fma_f32 v[16:17], v[180:181], v[16:17], v[20:21] op_sel_hi:[1,0,1]
	s_nop 0
	v_pk_mul_f32 v[18:19], v[28:29], v[16:17] op_sel:[1,1] op_sel_hi:[1,0] neg_lo:[1,0]
	v_add_u32_e32 v10, 0x1ff80, v13
	v_pk_fma_f32 v[16:17], v[28:29], v[16:17], v[18:19] op_sel_hi:[0,1,1]
	ds_write_b64 v10, v[16:17]
	v_mov_b32_e32 v10, v176
	v_mov_b32_e32 v13, v173
	s_waitcnt lgkmcnt(0)
	s_barrier
	v_mov_b32_e32 v16, v182
	v_add_u32_e32 v15, v13, v10
	v_lshl_add_u32 v75, v15, 3, 0
	v_xad_u32 v15, v13, 1, v10
	v_lshl_add_u32 v74, v15, 3, 0
	v_xad_u32 v15, v13, 2, v10
	v_lshl_add_u32 v73, v15, 3, 0
	v_xad_u32 v15, v13, 3, v10
	v_lshl_add_u32 v72, v15, 3, 0
	v_xad_u32 v15, v13, 4, v10
	v_lshl_add_u32 v71, v15, 3, 0
	v_xad_u32 v15, v13, 5, v10
	v_lshl_add_u32 v70, v15, 3, 0
	v_xad_u32 v15, v13, 6, v10
	v_lshl_add_u32 v69, v15, 3, 0
	v_xad_u32 v15, v13, 7, v10
	v_lshl_add_u32 v68, v15, 3, 0
	v_xad_u32 v15, v13, 8, v10
	v_lshl_add_u32 v15, v15, 3, 0
	v_add_u32_e32 v67, 0x800, v15
	v_xad_u32 v15, v13, 9, v10
	v_lshl_add_u32 v15, v15, 3, 0
	v_add_u32_e32 v66, 0x800, v15
	v_xad_u32 v15, v13, 10, v10
	v_lshl_add_u32 v15, v15, 3, 0
	v_add_u32_e32 v65, 0x800, v15
	v_xad_u32 v15, v13, 11, v10
	v_lshl_add_u32 v15, v15, 3, 0
	v_add_u32_e32 v64, 0x800, v15
	v_xad_u32 v15, v13, 12, v10
	v_mov_b32_e32 v17, v183
	v_lshl_add_u32 v15, v15, 3, 0
	ds_read2_b64 v[18:21], v75 offset1:16
	ds_read2_b64 v[40:43], v67 offset1:16
	v_add_u32_e32 v63, 0x800, v15
	v_xad_u32 v15, v13, 13, v10
	v_lshl_add_u32 v15, v15, 3, 0
	v_add_u32_e32 v62, 0x800, v15
	v_xad_u32 v15, v13, 14, v10
	v_xad_u32 v10, v13, 15, v10
	ds_read2_b64 v[22:25], v74 offset0:32 offset1:48
	ds_read2_b64 v[48:51], v66 offset0:32 offset1:48
	v_lshl_add_u32 v15, v15, 3, 0
	v_lshl_add_u32 v10, v10, 3, 0
	v_add_u32_e32 v15, 0x800, v15
	v_add_u32_e32 v13, 0x800, v10
	ds_read2_b64 v[26:29], v73 offset0:64 offset1:80
	ds_read2_b64 v[58:61], v72 offset0:96 offset1:112
	ds_read2_b64 v[76:79], v71 offset0:128 offset1:144
	ds_read2_b64 v[80:83], v70 offset0:160 offset1:176
	ds_read2_b64 v[84:87], v69 offset0:192 offset1:208
	ds_read2_b64 v[88:91], v68 offset0:224 offset1:240
	ds_read2_b64 v[54:57], v65 offset0:64 offset1:80
	ds_read2_b64 v[92:95], v64 offset0:96 offset1:112
	ds_read2_b64 v[96:99], v63 offset0:128 offset1:144
	ds_read2_b64 v[100:103], v62 offset0:160 offset1:176
	ds_read2_b64 v[104:107], v15 offset0:192 offset1:208
	ds_read2_b64 v[108:111], v13 offset0:224 offset1:240
	s_waitcnt lgkmcnt(14)
	v_pk_add_f32 v[112:113], v[18:19], v[40:41]
	v_pk_add_f32 v[40:41], v[18:19], v[40:41] neg_lo:[0,1] neg_hi:[0,1]
	v_pk_add_f32 v[18:19], v[20:21], v[42:43]
	v_pk_add_f32 v[20:21], v[20:21], v[42:43] neg_lo:[0,1] neg_hi:[0,1]
	v_mov_b32_e32 v30, v165
	v_mov_b32_e32 v32, v166
	v_mov_b32_e32 v34, v167
	v_mov_b32_e32 v10, v168
	v_mov_b32_e32 v38, v169
	v_mov_b32_e32 v36, v170
	v_mov_b32_e32 v46, v171
	v_mov_b32_e32 v31, v172
	v_pk_mul_f32 v[42:43], v[20:21], v[46:47] op_sel:[1,0] op_sel_hi:[0,0] neg_lo:[1,1] neg_hi:[0,1]
	s_nop 0
	v_pk_fma_f32 v[44:45], v[20:21], v[30:31], v[42:43] op_sel_hi:[1,0,1]
	s_waitcnt lgkmcnt(12)
	v_pk_add_f32 v[20:21], v[22:23], v[48:49]
	v_pk_add_f32 v[22:23], v[22:23], v[48:49] neg_lo:[0,1] neg_hi:[0,1]
	s_nop 0
	v_pk_mul_f32 v[42:43], v[22:23], v[36:37] op_sel:[1,0] op_sel_hi:[0,0] neg_lo:[1,1] neg_hi:[0,1]
	s_nop 0
	v_pk_fma_f32 v[48:49], v[22:23], v[32:33], v[42:43] op_sel_hi:[1,0,1]
	v_pk_add_f32 v[22:23], v[24:25], v[50:51]
	v_pk_add_f32 v[24:25], v[24:25], v[50:51] neg_lo:[0,1] neg_hi:[0,1]
	s_nop 0
	v_pk_mul_f32 v[42:43], v[24:25], v[38:39] op_sel:[1,0] op_sel_hi:[0,0] neg_lo:[1,1] neg_hi:[0,1]
	s_nop 0
	v_pk_fma_f32 v[52:53], v[24:25], v[34:35], v[42:43] op_sel_hi:[1,0,1]
	s_waitcnt lgkmcnt(5)
	v_pk_add_f32 v[24:25], v[26:27], v[54:55]
	v_pk_add_f32 v[26:27], v[26:27], v[54:55] neg_lo:[0,1] neg_hi:[0,1]
	s_nop 0
	v_pk_mul_f32 v[42:43], v[26:27], v[10:11] op_sel:[1,0] op_sel_hi:[0,0] neg_lo:[1,1] neg_hi:[0,1]
	s_nop 0
	v_pk_fma_f32 v[54:55], v[26:27], v[10:11], v[42:43] op_sel_hi:[1,0,1]
	v_pk_add_f32 v[26:27], v[28:29], v[56:57]
	v_pk_add_f32 v[28:29], v[28:29], v[56:57] neg_lo:[0,1] neg_hi:[0,1]
	s_nop 0
	v_pk_mul_f32 v[42:43], v[28:29], v[38:39] op_sel_hi:[1,0]
	s_nop 0
	v_pk_fma_f32 v[56:57], v[28:29], v[34:35], v[42:43] op_sel:[1,0,0] op_sel_hi:[0,0,1] neg_lo:[1,1,0] neg_hi:[0,1,0]
	s_waitcnt lgkmcnt(4)
	v_pk_add_f32 v[42:43], v[58:59], v[92:93] neg_lo:[0,1] neg_hi:[0,1]
	v_pk_add_f32 v[28:29], v[58:59], v[92:93]
	v_pk_mul_f32 v[50:51], v[42:43], v[36:37] op_sel_hi:[1,0]
	s_nop 0
	v_pk_fma_f32 v[58:59], v[42:43], v[32:33], v[50:51] op_sel:[1,0,0] op_sel_hi:[0,0,1] neg_lo:[1,1,0] neg_hi:[0,1,0]
	v_pk_add_f32 v[50:51], v[60:61], v[94:95] neg_lo:[0,1] neg_hi:[0,1]
	v_pk_add_f32 v[42:43], v[60:61], v[94:95]
	v_pk_mul_f32 v[60:61], v[50:51], v[46:47] op_sel_hi:[1,0]
	v_xor_b32_e32 v92, 0x80000000, v51
	v_mov_b32_e32 v93, v50
	s_waitcnt lgkmcnt(3)
	v_pk_add_f32 v[50:51], v[76:77], v[96:97]
	v_pk_add_f32 v[76:77], v[76:77], v[96:97] neg_lo:[0,1] neg_hi:[0,1]
	v_pk_fma_f32 v[60:61], v[92:93], v[30:31], v[60:61] op_sel_hi:[1,0,1] neg_lo:[0,1,0] neg_hi:[0,1,0]
	v_xor_b32_e32 v93, 0x80000000, v76
	v_mov_b32_e32 v92, v77
	v_pk_add_f32 v[76:77], v[78:79], v[98:99]
	v_pk_add_f32 v[78:79], v[78:79], v[98:99] neg_lo:[0,1] neg_hi:[0,1]
	s_nop 0
	v_pk_mul_f32 v[94:95], v[78:79], v[46:47] op_sel_hi:[1,0] neg_lo:[0,1] neg_hi:[0,1]
	s_nop 0
	v_pk_fma_f32 v[78:79], v[78:79], v[30:31], v[94:95] op_sel:[1,0,0] op_sel_hi:[0,0,1] neg_lo:[1,1,0] neg_hi:[0,1,0]
	s_waitcnt lgkmcnt(2)
	v_pk_add_f32 v[94:95], v[80:81], v[100:101]
	v_pk_add_f32 v[80:81], v[80:81], v[100:101] neg_lo:[0,1] neg_hi:[0,1]
	s_nop 0
	v_pk_mul_f32 v[96:97], v[80:81], v[36:37] op_sel_hi:[1,0] neg_lo:[0,1] neg_hi:[0,1]
	s_nop 0
	v_pk_fma_f32 v[80:81], v[80:81], v[32:33], v[96:97] op_sel:[1,0,0] op_sel_hi:[0,0,1] neg_lo:[1,1,0] neg_hi:[0,1,0]
	v_pk_add_f32 v[96:97], v[82:83], v[102:103]
	v_pk_add_f32 v[82:83], v[82:83], v[102:103] neg_lo:[0,1] neg_hi:[0,1]
	s_nop 0
	v_pk_mul_f32 v[98:99], v[82:83], v[38:39] op_sel_hi:[1,0] neg_lo:[0,1] neg_hi:[0,1]
	s_nop 0
	v_pk_fma_f32 v[82:83], v[82:83], v[34:35], v[98:99] op_sel:[1,0,0] op_sel_hi:[0,0,1] neg_lo:[1,1,0] neg_hi:[0,1,0]
	s_waitcnt lgkmcnt(1)
	v_pk_add_f32 v[98:99], v[84:85], v[104:105]
	v_pk_add_f32 v[84:85], v[84:85], v[104:105] neg_lo:[0,1] neg_hi:[0,1]
	s_nop 0
	v_pk_mul_f32 v[100:101], v[84:85], v[10:11] op_sel:[1,0] op_sel_hi:[0,0] neg_lo:[1,1] neg_hi:[0,1]
	s_nop 0
	v_pk_fma_f32 v[84:85], v[84:85], v[10:11], v[100:101] op_sel_hi:[1,0,1] neg_lo:[0,1,0] neg_hi:[0,1,0]
	v_pk_add_f32 v[100:101], v[86:87], v[106:107]
	v_pk_add_f32 v[86:87], v[86:87], v[106:107] neg_lo:[0,1] neg_hi:[0,1]
	s_nop 0
	v_pk_mul_f32 v[38:39], v[86:87], v[38:39] op_sel:[1,0] op_sel_hi:[0,0] neg_lo:[1,1] neg_hi:[0,1]
	s_nop 0
	v_pk_fma_f32 v[86:87], v[86:87], v[34:35], v[38:39] op_sel_hi:[1,0,1] neg_lo:[0,1,0] neg_hi:[0,1,0]
	s_waitcnt lgkmcnt(0)
	v_pk_add_f32 v[38:39], v[88:89], v[108:109] neg_lo:[0,1] neg_hi:[0,1]
	v_pk_add_f32 v[34:35], v[88:89], v[108:109]
	v_pk_mul_f32 v[88:89], v[38:39], v[36:37] op_sel:[1,0] op_sel_hi:[0,0] neg_lo:[1,1] neg_hi:[0,1]
	s_nop 0
	v_pk_fma_f32 v[88:89], v[38:39], v[32:33], v[88:89] op_sel_hi:[1,0,1] neg_lo:[0,1,0] neg_hi:[0,1,0]
	v_pk_add_f32 v[38:39], v[90:91], v[110:111]
	v_pk_add_f32 v[90:91], v[90:91], v[110:111] neg_lo:[0,1] neg_hi:[0,1]
	s_nop 0
	v_pk_mul_f32 v[46:47], v[90:91], v[46:47] op_sel:[1,0] op_sel_hi:[0,0] neg_lo:[1,1] neg_hi:[0,1]
	s_nop 0
	v_pk_fma_f32 v[90:91], v[90:91], v[30:31], v[46:47] op_sel_hi:[1,0,1] neg_lo:[0,1,0] neg_hi:[0,1,0]
	v_pk_add_f32 v[46:47], v[18:19], v[76:77]
	v_pk_add_f32 v[18:19], v[18:19], v[76:77] neg_lo:[0,1] neg_hi:[0,1]
	v_pk_add_f32 v[30:31], v[112:113], v[50:51]
	v_pk_mul_f32 v[76:77], v[18:19], v[36:37] op_sel:[1,0] op_sel_hi:[0,0] neg_lo:[1,1] neg_hi:[0,1]
	v_pk_add_f32 v[50:51], v[112:113], v[50:51] neg_lo:[0,1] neg_hi:[0,1]
	v_pk_fma_f32 v[76:77], v[18:19], v[32:33], v[76:77] op_sel_hi:[1,0,1]
	v_pk_add_f32 v[18:19], v[20:21], v[94:95]
	v_pk_add_f32 v[20:21], v[20:21], v[94:95] neg_lo:[0,1] neg_hi:[0,1]
	s_nop 0
	v_pk_mul_f32 v[94:95], v[20:21], v[10:11] op_sel:[1,0] op_sel_hi:[0,0] neg_lo:[1,1] neg_hi:[0,1]
	s_nop 0
	v_pk_fma_f32 v[20:21], v[20:21], v[10:11], v[94:95] op_sel_hi:[1,0,1]
	v_pk_add_f32 v[94:95], v[22:23], v[96:97]
	v_pk_add_f32 v[22:23], v[22:23], v[96:97] neg_lo:[0,1] neg_hi:[0,1]
	s_nop 0
	v_pk_mul_f32 v[96:97], v[22:23], v[36:37] op_sel_hi:[1,0]
	v_xor_b32_e32 v102, 0x80000000, v23
	v_mov_b32_e32 v103, v22
	v_pk_add_f32 v[22:23], v[24:25], v[98:99]
	v_pk_add_f32 v[24:25], v[24:25], v[98:99] neg_lo:[0,1] neg_hi:[0,1]
	v_pk_fma_f32 v[96:97], v[102:103], v[32:33], v[96:97] op_sel_hi:[1,0,1] neg_lo:[0,1,0] neg_hi:[0,1,0]
	v_xor_b32_e32 v99, 0x80000000, v24
	v_mov_b32_e32 v98, v25
	v_pk_add_f32 v[24:25], v[26:27], v[100:101]
	v_pk_add_f32 v[26:27], v[26:27], v[100:101] neg_lo:[0,1] neg_hi:[0,1]
	s_nop 0
	v_pk_mul_f32 v[100:101], v[26:27], v[36:37] op_sel_hi:[1,0] neg_lo:[0,1] neg_hi:[0,1]
	v_xor_b32_e32 v102, 0x80000000, v27
	v_mov_b32_e32 v103, v26
	v_pk_add_f32 v[26:27], v[28:29], v[34:35]
	v_pk_add_f32 v[28:29], v[28:29], v[34:35] neg_lo:[0,1] neg_hi:[0,1]
	v_pk_fma_f32 v[100:101], v[102:103], v[32:33], v[100:101] op_sel_hi:[1,0,1] neg_lo:[0,1,0] neg_hi:[0,1,0]
	v_pk_mul_f32 v[34:35], v[28:29], v[10:11] op_sel:[1,0] op_sel_hi:[0,0] neg_lo:[1,1] neg_hi:[0,1]
	v_pk_add_f32 v[102:103], v[30:31], v[22:23] neg_lo:[0,1] neg_hi:[0,1]
	v_pk_fma_f32 v[28:29], v[28:29], v[10:11], v[34:35] op_sel_hi:[1,0,1] neg_lo:[0,1,0] neg_hi:[0,1,0]
	v_pk_add_f32 v[34:35], v[42:43], v[38:39]
	v_pk_add_f32 v[38:39], v[42:43], v[38:39] neg_lo:[0,1] neg_hi:[0,1]
	s_nop 0
	v_pk_mul_f32 v[42:43], v[38:39], v[36:37] op_sel:[1,0] op_sel_hi:[0,0] neg_lo:[1,1] neg_hi:[0,1]
	s_nop 0
	v_pk_fma_f32 v[42:43], v[38:39], v[32:33], v[42:43] op_sel_hi:[1,0,1] neg_lo:[0,1,0] neg_hi:[0,1,0]
	v_pk_add_f32 v[38:39], v[30:31], v[22:23]
	v_pk_add_f32 v[22:23], v[46:47], v[24:25]
	v_pk_add_f32 v[24:25], v[46:47], v[24:25] neg_lo:[0,1] neg_hi:[0,1]
	s_nop 0
	v_pk_mul_f32 v[30:31], v[24:25], v[10:11] op_sel:[1,0] op_sel_hi:[0,0] neg_lo:[1,1] neg_hi:[0,1]
	s_nop 0
	v_pk_fma_f32 v[24:25], v[24:25], v[10:11], v[30:31] op_sel_hi:[1,0,1]
	v_pk_add_f32 v[30:31], v[18:19], v[26:27]
	v_pk_add_f32 v[18:19], v[18:19], v[26:27] neg_lo:[0,1] neg_hi:[0,1]
	s_nop 0
	v_xor_b32_e32 v27, 0x80000000, v18
	v_mov_b32_e32 v26, v19
	v_pk_add_f32 v[18:19], v[94:95], v[34:35]
	v_pk_add_f32 v[34:35], v[94:95], v[34:35] neg_lo:[0,1] neg_hi:[0,1]
	s_nop 0
	v_pk_mul_f32 v[46:47], v[34:35], v[10:11] op_sel:[1,0] op_sel_hi:[0,0] neg_lo:[1,1] neg_hi:[0,1]
	s_nop 0
	v_pk_fma_f32 v[34:35], v[34:35], v[10:11], v[46:47] op_sel_hi:[1,0,1] neg_lo:[0,1,0] neg_hi:[0,1,0]
	v_pk_add_f32 v[46:47], v[38:39], v[30:31]
	v_pk_add_f32 v[38:39], v[38:39], v[30:31] neg_lo:[0,1] neg_hi:[0,1]
	v_pk_add_f32 v[30:31], v[22:23], v[18:19]
	v_pk_add_f32 v[18:19], v[22:23], v[18:19] neg_lo:[0,1] neg_hi:[0,1]
	v_pk_add_f32 v[94:95], v[46:47], v[30:31]
	v_xor_b32_e32 v23, 0x80000000, v18
	v_mov_b32_e32 v22, v19
	v_pk_add_f32 v[18:19], v[102:103], v[26:27]
	v_pk_add_f32 v[102:103], v[102:103], v[26:27] neg_lo:[0,1] neg_hi:[0,1]
	v_pk_add_f32 v[26:27], v[24:25], v[34:35]
	v_pk_add_f32 v[24:25], v[24:25], v[34:35] neg_lo:[0,1] neg_hi:[0,1]
	v_pk_add_f32 v[30:31], v[46:47], v[30:31] neg_lo:[0,1] neg_hi:[0,1]
	v_xor_b32_e32 v35, 0x80000000, v24
	v_mov_b32_e32 v34, v25
	v_pk_add_f32 v[24:25], v[50:51], v[98:99]
	v_pk_add_f32 v[98:99], v[50:51], v[98:99] neg_lo:[0,1] neg_hi:[0,1]
	v_pk_add_f32 v[50:51], v[76:77], v[100:101] neg_lo:[0,1] neg_hi:[0,1]
	v_pk_add_f32 v[46:47], v[38:39], v[22:23]
	v_pk_add_f32 v[22:23], v[38:39], v[22:23] neg_lo:[0,1] neg_hi:[0,1]
	v_pk_add_f32 v[104:105], v[18:19], v[26:27]
	v_pk_add_f32 v[26:27], v[18:19], v[26:27] neg_lo:[0,1] neg_hi:[0,1]
	v_pk_add_f32 v[38:39], v[102:103], v[34:35]
	v_pk_add_f32 v[18:19], v[102:103], v[34:35] neg_lo:[0,1] neg_hi:[0,1]
	v_pk_add_f32 v[34:35], v[76:77], v[100:101]
	v_pk_mul_f32 v[76:77], v[10:11], v[50:51] op_sel:[0,1] op_sel_hi:[0,0] neg_lo:[1,1] neg_hi:[1,0]
	v_pk_fma_f32 v[76:77], v[10:11], v[50:51], v[76:77] op_sel_hi:[0,1,1]
	v_pk_add_f32 v[50:51], v[20:21], v[28:29]
	v_pk_add_f32 v[20:21], v[20:21], v[28:29] neg_lo:[0,1] neg_hi:[0,1]
	s_nop 0
	v_xor_b32_e32 v29, 0x80000000, v20
	v_mov_b32_e32 v28, v21
	v_pk_add_f32 v[20:21], v[96:97], v[42:43]
	v_pk_add_f32 v[42:43], v[96:97], v[42:43] neg_lo:[0,1] neg_hi:[0,1]
	s_nop 0
	v_pk_mul_f32 v[96:97], v[10:11], v[42:43] op_sel:[0,1] op_sel_hi:[0,0] neg_lo:[1,1] neg_hi:[1,0]
	v_pk_fma_f32 v[42:43], v[10:11], v[42:43], v[96:97] op_sel_hi:[0,1,1] neg_lo:[1,0,0] neg_hi:[1,0,0]
	v_pk_add_f32 v[96:97], v[24:25], v[50:51]
	v_pk_add_f32 v[24:25], v[24:25], v[50:51] neg_lo:[0,1] neg_hi:[0,1]
	v_pk_add_f32 v[50:51], v[34:35], v[20:21]
	v_pk_add_f32 v[20:21], v[34:35], v[20:21] neg_lo:[0,1] neg_hi:[0,1]
	v_pk_add_f32 v[102:103], v[96:97], v[50:51]
	v_xor_b32_e32 v101, 0x80000000, v20
	v_mov_b32_e32 v100, v21
	v_pk_add_f32 v[34:35], v[96:97], v[50:51] neg_lo:[0,1] neg_hi:[0,1]
	v_pk_add_f32 v[20:21], v[98:99], v[28:29]
	v_pk_add_f32 v[96:97], v[98:99], v[28:29] neg_lo:[0,1] neg_hi:[0,1]
	v_pk_add_f32 v[28:29], v[76:77], v[42:43]
	v_pk_add_f32 v[42:43], v[76:77], v[42:43] neg_lo:[0,1] neg_hi:[0,1]
	v_pk_add_f32 v[98:99], v[20:21], v[28:29]
	v_xor_b32_e32 v77, 0x80000000, v42
	v_mov_b32_e32 v76, v43
	v_pk_add_f32 v[28:29], v[20:21], v[28:29] neg_lo:[0,1] neg_hi:[0,1]
	v_pk_add_f32 v[42:43], v[96:97], v[76:77]
	v_pk_add_f32 v[20:21], v[96:97], v[76:77] neg_lo:[0,1] neg_hi:[0,1]
	v_pk_add_f32 v[76:77], v[40:41], v[92:93]
	v_pk_add_f32 v[92:93], v[40:41], v[92:93] neg_lo:[0,1] neg_hi:[0,1]
	v_pk_add_f32 v[40:41], v[44:45], v[78:79]
	v_pk_add_f32 v[44:45], v[44:45], v[78:79] neg_lo:[0,1] neg_hi:[0,1]
	v_pk_add_f32 v[50:51], v[24:25], v[100:101]
	v_pk_mul_f32 v[78:79], v[36:37], v[44:45] op_sel:[0,1] op_sel_hi:[0,0] neg_lo:[1,1] neg_hi:[1,0]
	v_pk_fma_f32 v[44:45], v[32:33], v[44:45], v[78:79] op_sel_hi:[0,1,1]
	v_pk_add_f32 v[78:79], v[48:49], v[80:81]
	v_pk_add_f32 v[48:49], v[48:49], v[80:81] neg_lo:[0,1] neg_hi:[0,1]
	v_pk_add_f32 v[24:25], v[24:25], v[100:101] neg_lo:[0,1] neg_hi:[0,1]
	v_pk_mul_f32 v[80:81], v[10:11], v[48:49] op_sel:[0,1] op_sel_hi:[0,0] neg_lo:[1,1] neg_hi:[1,0]
	v_pk_fma_f32 v[80:81], v[10:11], v[48:49], v[80:81] op_sel_hi:[0,1,1]
	v_pk_add_f32 v[48:49], v[52:53], v[82:83]
	v_pk_add_f32 v[52:53], v[52:53], v[82:83] neg_lo:[0,1] neg_hi:[0,1]
	s_nop 0
	v_pk_mul_f32 v[82:83], v[32:33], v[52:53] op_sel:[0,1] op_sel_hi:[0,0] neg_lo:[1,1] neg_hi:[1,0]
	v_pk_fma_f32 v[52:53], v[36:37], v[52:53], v[82:83] op_sel_hi:[0,1,1]
	v_pk_add_f32 v[82:83], v[54:55], v[84:85]
	v_pk_add_f32 v[54:55], v[54:55], v[84:85] neg_lo:[0,1] neg_hi:[0,1]
	s_nop 0
	v_xor_b32_e32 v85, 0x80000000, v54
	v_mov_b32_e32 v84, v55
	v_pk_add_f32 v[54:55], v[56:57], v[86:87]
	v_pk_add_f32 v[56:57], v[56:57], v[86:87] neg_lo:[0,1] neg_hi:[0,1]
	s_nop 0
	v_pk_mul_f32 v[86:87], v[32:33], v[56:57] op_sel:[0,1] op_sel_hi:[0,0] neg_lo:[1,1] neg_hi:[1,0]
	v_pk_fma_f32 v[56:57], v[36:37], v[56:57], v[86:87] op_sel_hi:[0,1,1] neg_lo:[1,0,0] neg_hi:[1,0,0]
	v_pk_add_f32 v[86:87], v[58:59], v[88:89]
	v_pk_add_f32 v[58:59], v[58:59], v[88:89] neg_lo:[0,1] neg_hi:[0,1]
	s_nop 0
	v_pk_mul_f32 v[88:89], v[10:11], v[58:59] op_sel:[0,1] op_sel_hi:[0,0] neg_lo:[1,1] neg_hi:[1,0]
	v_pk_fma_f32 v[58:59], v[10:11], v[58:59], v[88:89] op_sel_hi:[0,1,1] neg_lo:[1,0,0] neg_hi:[1,0,0]
	v_pk_add_f32 v[88:89], v[60:61], v[90:91]
	v_pk_add_f32 v[60:61], v[60:61], v[90:91] neg_lo:[0,1] neg_hi:[0,1]
	s_nop 0
	v_pk_mul_f32 v[36:37], v[36:37], v[60:61] op_sel:[0,1] op_sel_hi:[0,0] neg_lo:[1,1] neg_hi:[1,0]
	v_pk_fma_f32 v[36:37], v[32:33], v[60:61], v[36:37] op_sel_hi:[0,1,1] neg_lo:[1,0,0] neg_hi:[1,0,0]
	v_pk_add_f32 v[32:33], v[76:77], v[82:83]
	v_pk_add_f32 v[60:61], v[76:77], v[82:83] neg_lo:[0,1] neg_hi:[0,1]
	v_pk_add_f32 v[76:77], v[54:55], v[40:41]
	v_pk_add_f32 v[40:41], v[40:41], v[54:55] neg_lo:[0,1] neg_hi:[0,1]
	s_nop 0
	v_pk_mul_f32 v[54:55], v[10:11], v[40:41] op_sel:[0,1] op_sel_hi:[0,0] neg_lo:[1,1] neg_hi:[1,0]
	v_pk_fma_f32 v[54:55], v[10:11], v[40:41], v[54:55] op_sel_hi:[0,1,1]
	v_pk_add_f32 v[40:41], v[78:79], v[86:87]
	v_pk_add_f32 v[78:79], v[78:79], v[86:87] neg_lo:[0,1] neg_hi:[0,1]
	s_nop 0
	v_xor_b32_e32 v83, 0x80000000, v78
	v_mov_b32_e32 v82, v79
	v_pk_add_f32 v[78:79], v[48:49], v[88:89]
	v_pk_add_f32 v[48:49], v[48:49], v[88:89] neg_lo:[0,1] neg_hi:[0,1]
	v_pk_add_f32 v[88:89], v[76:77], v[78:79]
	v_pk_mul_f32 v[86:87], v[10:11], v[48:49] op_sel:[0,1] op_sel_hi:[0,0] neg_lo:[1,1] neg_hi:[1,0]
	v_pk_fma_f32 v[48:49], v[10:11], v[48:49], v[86:87] op_sel_hi:[0,1,1] neg_lo:[1,0,0] neg_hi:[1,0,0]
	v_pk_add_f32 v[86:87], v[32:33], v[40:41]
	v_pk_add_f32 v[32:33], v[32:33], v[40:41] neg_lo:[0,1] neg_hi:[0,1]
	v_pk_add_f32 v[40:41], v[76:77], v[78:79] neg_lo:[0,1] neg_hi:[0,1]
	v_pk_add_f32 v[78:79], v[86:87], v[88:89] neg_lo:[0,1] neg_hi:[0,1]
	v_pk_add_f32 v[90:91], v[32:33], v[40:41] op_sel:[0,1] op_sel_hi:[1,0] neg_hi:[0,1]
	v_pk_add_f32 v[40:41], v[32:33], v[40:41] op_sel:[0,1] op_sel_hi:[1,0] neg_lo:[0,1]
	v_pk_add_f32 v[76:77], v[54:55], v[48:49]
	v_pk_add_f32 v[48:49], v[54:55], v[48:49] neg_lo:[0,1] neg_hi:[0,1]
	v_pk_add_f32 v[32:33], v[60:61], v[82:83]
	v_pk_add_f32 v[60:61], v[60:61], v[82:83] neg_lo:[0,1] neg_hi:[0,1]
	v_xor_b32_e32 v55, 0x80000000, v48
	v_mov_b32_e32 v54, v49
	v_pk_add_f32 v[82:83], v[32:33], v[76:77]
	v_pk_add_f32 v[48:49], v[32:33], v[76:77] neg_lo:[0,1] neg_hi:[0,1]
	v_pk_add_f32 v[76:77], v[60:61], v[54:55]
	v_pk_add_f32 v[32:33], v[60:61], v[54:55] neg_lo:[0,1] neg_hi:[0,1]
	v_pk_add_f32 v[54:55], v[92:93], v[84:85]
	v_pk_add_f32 v[60:61], v[92:93], v[84:85] neg_lo:[0,1] neg_hi:[0,1]
	v_pk_add_f32 v[84:85], v[56:57], v[44:45]
	v_pk_add_f32 v[44:45], v[44:45], v[56:57] neg_lo:[0,1] neg_hi:[0,1]
	v_pk_add_f32 v[86:87], v[86:87], v[88:89]
	v_pk_mul_f32 v[56:57], v[10:11], v[44:45] op_sel:[0,1] op_sel_hi:[0,0] neg_lo:[1,1] neg_hi:[1,0]
	v_pk_fma_f32 v[56:57], v[10:11], v[44:45], v[56:57] op_sel_hi:[0,1,1]
	v_pk_add_f32 v[44:45], v[80:81], v[58:59]
	v_pk_add_f32 v[58:59], v[80:81], v[58:59] neg_lo:[0,1] neg_hi:[0,1]
	s_nop 0
	v_xor_b32_e32 v81, 0x80000000, v58
	v_mov_b32_e32 v80, v59
	v_pk_add_f32 v[58:59], v[52:53], v[36:37]
	v_pk_add_f32 v[36:37], v[52:53], v[36:37] neg_lo:[0,1] neg_hi:[0,1]
	s_nop 0
	v_pk_mul_f32 v[52:53], v[10:11], v[36:37] op_sel:[0,1] op_sel_hi:[0,0] neg_lo:[1,1] neg_hi:[1,0]
	v_pk_fma_f32 v[36:37], v[10:11], v[36:37], v[52:53] op_sel_hi:[0,1,1] neg_lo:[1,0,0] neg_hi:[1,0,0]
	v_pk_add_f32 v[52:53], v[54:55], v[44:45]
	v_pk_add_f32 v[44:45], v[54:55], v[44:45] neg_lo:[0,1] neg_hi:[0,1]
	v_pk_add_f32 v[54:55], v[84:85], v[58:59]
	v_pk_add_f32 v[58:59], v[84:85], v[58:59] neg_lo:[0,1] neg_hi:[0,1]
	s_nop 0
	v_xor_b32_e32 v85, 0x80000000, v58
	v_mov_b32_e32 v84, v59
	v_pk_add_f32 v[58:59], v[52:53], v[54:55]
	v_pk_add_f32 v[52:53], v[52:53], v[54:55] neg_lo:[0,1] neg_hi:[0,1]
	v_pk_add_f32 v[54:55], v[44:45], v[84:85]
	v_pk_add_f32 v[44:45], v[44:45], v[84:85] neg_lo:[0,1] neg_hi:[0,1]
	v_pk_add_f32 v[84:85], v[60:61], v[80:81]
	v_pk_add_f32 v[60:61], v[60:61], v[80:81] neg_lo:[0,1] neg_hi:[0,1]
	v_pk_add_f32 v[80:81], v[56:57], v[36:37]
	v_pk_add_f32 v[36:37], v[56:57], v[36:37] neg_lo:[0,1] neg_hi:[0,1]
	v_pk_add_f32 v[92:93], v[84:85], v[80:81]
	v_pk_add_f32 v[80:81], v[84:85], v[80:81] neg_lo:[0,1] neg_hi:[0,1]
	v_pk_add_f32 v[84:85], v[60:61], v[36:37] op_sel:[0,1] op_sel_hi:[1,0] neg_hi:[0,1]
	v_pk_add_f32 v[36:37], v[60:61], v[36:37] op_sel:[0,1] op_sel_hi:[1,0] neg_lo:[0,1]
	v_pk_fma_f32 v[60:61], v[16:17], s[92:93], v[16:17] op_sel:[1,0,0] op_sel_hi:[0,1,1]
	v_pk_mul_f32 v[56:57], v[94:95], s[14:15] op_sel:[1,0] neg_lo:[1,0]
	v_pk_mul_f32 v[88:89], v[60:61], v[86:87] op_sel:[1,1] op_sel_hi:[0,1] neg_lo:[0,1]
	v_pk_fma_f32 v[56:57], v[94:95], s[42:43], v[56:57] op_sel_hi:[0,1,1]
	v_pk_fma_f32 v[86:87], v[60:61], v[86:87], v[88:89] op_sel_hi:[1,0,1]
	ds_write2_b64 v75, v[56:57], v[86:87] offset1:16
	v_pk_mul_f32 v[56:57], v[16:17], v[60:61] op_sel:[1,1] op_sel_hi:[0,1] neg_lo:[0,1]
	v_pk_fma_f32 v[56:57], v[16:17], v[60:61], v[56:57] op_sel_hi:[1,0,1]
	s_nop 0
	v_pk_mul_f32 v[60:61], v[56:57], v[102:103] op_sel:[1,1] op_sel_hi:[0,1] neg_lo:[0,1]
	v_pk_mul_f32 v[86:87], v[16:17], v[56:57] op_sel:[1,1] op_sel_hi:[0,1] neg_lo:[0,1]
	v_pk_fma_f32 v[60:61], v[56:57], v[102:103], v[60:61] op_sel_hi:[1,0,1]
	v_pk_fma_f32 v[56:57], v[16:17], v[56:57], v[86:87] op_sel_hi:[1,0,1]
	s_nop 0
	v_pk_mul_f32 v[86:87], v[56:57], v[58:59] op_sel:[1,1] op_sel_hi:[0,1] neg_lo:[0,1]
	v_pk_fma_f32 v[58:59], v[56:57], v[58:59], v[86:87] op_sel_hi:[1,0,1]
	ds_write2_b64 v74, v[60:61], v[58:59] offset0:32 offset1:48
	v_pk_mul_f32 v[58:59], v[16:17], v[56:57] op_sel:[1,1] op_sel_hi:[0,1] neg_lo:[0,1]
	v_pk_fma_f32 v[56:57], v[16:17], v[56:57], v[58:59] op_sel_hi:[1,0,1]
	s_nop 0
	v_pk_mul_f32 v[58:59], v[56:57], v[104:105] op_sel:[1,1] op_sel_hi:[0,1] neg_lo:[0,1]
	v_pk_mul_f32 v[60:61], v[16:17], v[56:57] op_sel:[1,1] op_sel_hi:[0,1] neg_lo:[0,1]
	v_pk_fma_f32 v[58:59], v[56:57], v[104:105], v[58:59] op_sel_hi:[1,0,1]
	v_pk_fma_f32 v[56:57], v[16:17], v[56:57], v[60:61] op_sel_hi:[1,0,1]
	s_nop 0
	v_pk_mul_f32 v[60:61], v[56:57], v[82:83] op_sel:[1,1] op_sel_hi:[0,1] neg_lo:[0,1]
	v_pk_fma_f32 v[60:61], v[56:57], v[82:83], v[60:61] op_sel_hi:[1,0,1]
	ds_write2_b64 v73, v[58:59], v[60:61] offset0:64 offset1:80
	v_pk_mul_f32 v[58:59], v[16:17], v[56:57] op_sel:[1,1] op_sel_hi:[0,1] neg_lo:[0,1]
	v_pk_fma_f32 v[56:57], v[16:17], v[56:57], v[58:59] op_sel_hi:[1,0,1]
	s_nop 0
	v_pk_mul_f32 v[58:59], v[56:57], v[98:99] op_sel:[1,1] op_sel_hi:[0,1] neg_lo:[0,1]
	v_pk_mul_f32 v[60:61], v[16:17], v[56:57] op_sel:[1,1] op_sel_hi:[0,1] neg_lo:[0,1]
	v_pk_fma_f32 v[58:59], v[56:57], v[98:99], v[58:59] op_sel_hi:[1,0,1]
	v_pk_fma_f32 v[56:57], v[16:17], v[56:57], v[60:61] op_sel_hi:[1,0,1]
	s_nop 0
	v_pk_mul_f32 v[60:61], v[56:57], v[92:93] op_sel:[1,1] op_sel_hi:[0,1] neg_lo:[0,1]
	v_pk_fma_f32 v[60:61], v[56:57], v[92:93], v[60:61] op_sel_hi:[1,0,1]
	ds_write2_b64 v72, v[58:59], v[60:61] offset0:96 offset1:112
	v_pk_mul_f32 v[58:59], v[16:17], v[56:57] op_sel:[1,1] op_sel_hi:[0,1] neg_lo:[0,1]
	v_pk_fma_f32 v[56:57], v[16:17], v[56:57], v[58:59] op_sel_hi:[1,0,1]
	s_nop 0
	v_pk_mul_f32 v[58:59], v[56:57], v[46:47] op_sel:[1,1] op_sel_hi:[0,1] neg_lo:[0,1]
	v_pk_fma_f32 v[46:47], v[56:57], v[46:47], v[58:59] op_sel_hi:[1,0,1]
	v_pk_mul_f32 v[58:59], v[16:17], v[56:57] op_sel:[1,1] op_sel_hi:[0,1] neg_lo:[0,1]
	v_pk_fma_f32 v[56:57], v[16:17], v[56:57], v[58:59] op_sel_hi:[1,0,1]
	s_nop 0
	v_pk_mul_f32 v[58:59], v[56:57], v[90:91] op_sel:[1,1] op_sel_hi:[0,1] neg_lo:[0,1]
	v_pk_fma_f32 v[58:59], v[56:57], v[90:91], v[58:59] op_sel_hi:[1,0,1]
	ds_write2_b64 v71, v[46:47], v[58:59] offset0:128 offset1:144
	v_pk_mul_f32 v[46:47], v[16:17], v[56:57] op_sel:[1,1] op_sel_hi:[0,1] neg_lo:[0,1]
	v_pk_fma_f32 v[46:47], v[16:17], v[56:57], v[46:47] op_sel_hi:[1,0,1]
	s_nop 0
	v_pk_mul_f32 v[56:57], v[46:47], v[50:51] op_sel:[1,1] op_sel_hi:[0,1] neg_lo:[0,1]
	v_pk_fma_f32 v[50:51], v[46:47], v[50:51], v[56:57] op_sel_hi:[1,0,1]
	v_pk_mul_f32 v[56:57], v[16:17], v[46:47] op_sel:[1,1] op_sel_hi:[0,1] neg_lo:[0,1]
	v_pk_fma_f32 v[46:47], v[16:17], v[46:47], v[56:57] op_sel_hi:[1,0,1]
	s_nop 0
	v_pk_mul_f32 v[56:57], v[46:47], v[54:55] op_sel:[1,1] op_sel_hi:[0,1] neg_lo:[0,1]
	v_pk_fma_f32 v[54:55], v[46:47], v[54:55], v[56:57] op_sel_hi:[1,0,1]
	ds_write2_b64 v70, v[50:51], v[54:55] offset0:160 offset1:176
	v_pk_mul_f32 v[50:51], v[16:17], v[46:47] op_sel:[1,1] op_sel_hi:[0,1] neg_lo:[0,1]
	v_pk_fma_f32 v[46:47], v[16:17], v[46:47], v[50:51] op_sel_hi:[1,0,1]
	s_nop 0
	v_pk_mul_f32 v[50:51], v[38:39], v[46:47] op_sel:[1,1] op_sel_hi:[1,0] neg_lo:[1,0]
	s_nop 0
	v_pk_fma_f32 v[38:39], v[38:39], v[46:47], v[50:51] op_sel_hi:[0,1,1]
	v_pk_mul_f32 v[50:51], v[16:17], v[46:47] op_sel:[1,1] op_sel_hi:[0,1] neg_lo:[0,1]
	v_pk_fma_f32 v[46:47], v[16:17], v[46:47], v[50:51] op_sel_hi:[1,0,1]
	s_nop 0
	v_pk_mul_f32 v[50:51], v[46:47], v[76:77] op_sel:[1,1] op_sel_hi:[0,1] neg_lo:[0,1]
	v_pk_fma_f32 v[50:51], v[46:47], v[76:77], v[50:51] op_sel_hi:[1,0,1]
	ds_write2_b64 v69, v[38:39], v[50:51] offset0:192 offset1:208
	v_pk_mul_f32 v[38:39], v[16:17], v[46:47] op_sel:[1,1] op_sel_hi:[0,1] neg_lo:[0,1]
	v_pk_fma_f32 v[38:39], v[16:17], v[46:47], v[38:39] op_sel_hi:[1,0,1]
	s_nop 0
	v_pk_mul_f32 v[46:47], v[42:43], v[38:39] op_sel:[1,1] op_sel_hi:[1,0] neg_lo:[1,0]
	s_nop 0
	v_pk_fma_f32 v[42:43], v[42:43], v[38:39], v[46:47] op_sel_hi:[0,1,1]
	v_pk_mul_f32 v[46:47], v[16:17], v[38:39] op_sel:[1,1] op_sel_hi:[0,1] neg_lo:[0,1]
	v_pk_fma_f32 v[38:39], v[16:17], v[38:39], v[46:47] op_sel_hi:[1,0,1]
	s_nop 0
	v_pk_mul_f32 v[46:47], v[38:39], v[84:85] op_sel:[1,1] op_sel_hi:[0,1] neg_lo:[0,1]
	v_pk_fma_f32 v[46:47], v[38:39], v[84:85], v[46:47] op_sel_hi:[1,0,1]
	ds_write2_b64 v68, v[42:43], v[46:47] offset0:224 offset1:240
	v_pk_mul_f32 v[42:43], v[16:17], v[38:39] op_sel:[1,1] op_sel_hi:[0,1] neg_lo:[0,1]
	v_pk_fma_f32 v[38:39], v[16:17], v[38:39], v[42:43] op_sel_hi:[1,0,1]
	s_nop 0
	v_pk_mul_f32 v[42:43], v[30:31], v[38:39] op_sel:[1,1] op_sel_hi:[1,0] neg_lo:[1,0]
	s_nop 0
	v_pk_fma_f32 v[30:31], v[30:31], v[38:39], v[42:43] op_sel_hi:[0,1,1]
	v_pk_mul_f32 v[42:43], v[16:17], v[38:39] op_sel:[1,1] op_sel_hi:[0,1] neg_lo:[0,1]
	v_pk_fma_f32 v[38:39], v[16:17], v[38:39], v[42:43] op_sel_hi:[1,0,1]
	s_nop 0
	v_pk_mul_f32 v[42:43], v[78:79], v[38:39] op_sel:[1,1] op_sel_hi:[1,0] neg_lo:[1,0]
	s_nop 0
	v_pk_fma_f32 v[42:43], v[78:79], v[38:39], v[42:43] op_sel_hi:[0,1,1]
	ds_write2_b64 v67, v[30:31], v[42:43] offset1:16
	v_pk_mul_f32 v[30:31], v[16:17], v[38:39] op_sel:[1,1] op_sel_hi:[0,1] neg_lo:[0,1]
	v_pk_fma_f32 v[30:31], v[16:17], v[38:39], v[30:31] op_sel_hi:[1,0,1]
	s_nop 0
	v_pk_mul_f32 v[38:39], v[34:35], v[30:31] op_sel:[1,1] op_sel_hi:[1,0] neg_lo:[1,0]
	s_nop 0
	v_pk_fma_f32 v[34:35], v[34:35], v[30:31], v[38:39] op_sel_hi:[0,1,1]
	v_pk_mul_f32 v[38:39], v[16:17], v[30:31] op_sel:[1,1] op_sel_hi:[0,1] neg_lo:[0,1]
	v_pk_fma_f32 v[30:31], v[16:17], v[30:31], v[38:39] op_sel_hi:[1,0,1]
	s_nop 0
	v_pk_mul_f32 v[38:39], v[52:53], v[30:31] op_sel:[1,1] op_sel_hi:[1,0] neg_lo:[1,0]
	s_nop 0
	v_pk_fma_f32 v[38:39], v[52:53], v[30:31], v[38:39] op_sel_hi:[0,1,1]
	ds_write2_b64 v66, v[34:35], v[38:39] offset0:32 offset1:48
	v_pk_mul_f32 v[34:35], v[16:17], v[30:31] op_sel:[1,1] op_sel_hi:[0,1] neg_lo:[0,1]
	v_pk_fma_f32 v[30:31], v[16:17], v[30:31], v[34:35] op_sel_hi:[1,0,1]
	s_nop 0
	v_pk_mul_f32 v[34:35], v[26:27], v[30:31] op_sel:[1,1] op_sel_hi:[1,0] neg_lo:[1,0]
	s_nop 0
	v_pk_fma_f32 v[26:27], v[26:27], v[30:31], v[34:35] op_sel_hi:[0,1,1]
	v_pk_mul_f32 v[34:35], v[16:17], v[30:31] op_sel:[1,1] op_sel_hi:[0,1] neg_lo:[0,1]
	v_pk_fma_f32 v[30:31], v[16:17], v[30:31], v[34:35] op_sel_hi:[1,0,1]
	s_nop 0
	v_pk_mul_f32 v[34:35], v[48:49], v[30:31] op_sel:[1,1] op_sel_hi:[1,0] neg_lo:[1,0]
	s_nop 0
	v_pk_fma_f32 v[34:35], v[48:49], v[30:31], v[34:35] op_sel_hi:[0,1,1]
	ds_write2_b64 v65, v[26:27], v[34:35] offset0:64 offset1:80
	v_pk_mul_f32 v[26:27], v[16:17], v[30:31] op_sel:[1,1] op_sel_hi:[0,1] neg_lo:[0,1]
	v_pk_fma_f32 v[26:27], v[16:17], v[30:31], v[26:27] op_sel_hi:[1,0,1]
	s_nop 0
	v_pk_mul_f32 v[30:31], v[28:29], v[26:27] op_sel:[1,1] op_sel_hi:[1,0] neg_lo:[1,0]
	s_nop 0
	v_pk_fma_f32 v[28:29], v[28:29], v[26:27], v[30:31] op_sel_hi:[0,1,1]
	v_pk_mul_f32 v[30:31], v[16:17], v[26:27] op_sel:[1,1] op_sel_hi:[0,1] neg_lo:[0,1]
	v_pk_fma_f32 v[26:27], v[16:17], v[26:27], v[30:31] op_sel_hi:[1,0,1]
	s_nop 0
	v_pk_mul_f32 v[30:31], v[80:81], v[26:27] op_sel:[1,1] op_sel_hi:[1,0] neg_lo:[1,0]
	s_nop 0
	v_pk_fma_f32 v[30:31], v[80:81], v[26:27], v[30:31] op_sel_hi:[0,1,1]
	ds_write2_b64 v64, v[28:29], v[30:31] offset0:96 offset1:112
	v_pk_mul_f32 v[28:29], v[16:17], v[26:27] op_sel:[1,1] op_sel_hi:[0,1] neg_lo:[0,1]
	v_pk_fma_f32 v[26:27], v[16:17], v[26:27], v[28:29] op_sel_hi:[1,0,1]
	s_nop 0
	v_pk_mul_f32 v[28:29], v[22:23], v[26:27] op_sel:[1,1] op_sel_hi:[1,0] neg_lo:[1,0]
	s_nop 0
	v_pk_fma_f32 v[22:23], v[22:23], v[26:27], v[28:29] op_sel_hi:[0,1,1]
	v_pk_mul_f32 v[28:29], v[16:17], v[26:27] op_sel:[1,1] op_sel_hi:[0,1] neg_lo:[0,1]
	v_pk_fma_f32 v[26:27], v[16:17], v[26:27], v[28:29] op_sel_hi:[1,0,1]
	s_nop 0
	v_pk_mul_f32 v[28:29], v[40:41], v[26:27] op_sel:[1,1] op_sel_hi:[1,0] neg_lo:[1,0]
	s_nop 0
	v_pk_fma_f32 v[28:29], v[40:41], v[26:27], v[28:29] op_sel_hi:[0,1,1]
	ds_write2_b64 v63, v[22:23], v[28:29] offset0:128 offset1:144
	v_pk_mul_f32 v[22:23], v[16:17], v[26:27] op_sel:[1,1] op_sel_hi:[0,1] neg_lo:[0,1]
	v_pk_fma_f32 v[22:23], v[16:17], v[26:27], v[22:23] op_sel_hi:[1,0,1]
	s_nop 0
	v_pk_mul_f32 v[26:27], v[24:25], v[22:23] op_sel:[1,1] op_sel_hi:[1,0] neg_lo:[1,0]
	s_nop 0
	v_pk_fma_f32 v[24:25], v[24:25], v[22:23], v[26:27] op_sel_hi:[0,1,1]
	v_pk_mul_f32 v[26:27], v[16:17], v[22:23] op_sel:[1,1] op_sel_hi:[0,1] neg_lo:[0,1]
	v_pk_fma_f32 v[22:23], v[16:17], v[22:23], v[26:27] op_sel_hi:[1,0,1]
	s_nop 0
	v_pk_mul_f32 v[26:27], v[44:45], v[22:23] op_sel:[1,1] op_sel_hi:[1,0] neg_lo:[1,0]
	s_nop 0
	v_pk_fma_f32 v[26:27], v[44:45], v[22:23], v[26:27] op_sel_hi:[0,1,1]
	ds_write2_b64 v62, v[24:25], v[26:27] offset0:160 offset1:176
	v_pk_mul_f32 v[24:25], v[16:17], v[22:23] op_sel:[1,1] op_sel_hi:[0,1] neg_lo:[0,1]
	v_pk_fma_f32 v[22:23], v[16:17], v[22:23], v[24:25] op_sel_hi:[1,0,1]
	s_nop 0
	v_pk_mul_f32 v[24:25], v[18:19], v[22:23] op_sel:[1,1] op_sel_hi:[1,0] neg_lo:[1,0]
	s_nop 0
	v_pk_fma_f32 v[18:19], v[18:19], v[22:23], v[24:25] op_sel_hi:[0,1,1]
	v_pk_mul_f32 v[24:25], v[16:17], v[22:23] op_sel:[1,1] op_sel_hi:[0,1] neg_lo:[0,1]
	v_pk_fma_f32 v[22:23], v[16:17], v[22:23], v[24:25] op_sel_hi:[1,0,1]
	s_nop 0
	v_pk_mul_f32 v[24:25], v[32:33], v[22:23] op_sel:[1,1] op_sel_hi:[1,0] neg_lo:[1,0]
	s_nop 0
	v_pk_fma_f32 v[24:25], v[32:33], v[22:23], v[24:25] op_sel_hi:[0,1,1]
	ds_write2_b64 v15, v[18:19], v[24:25] offset0:192 offset1:208
	v_pk_mul_f32 v[18:19], v[16:17], v[22:23] op_sel:[1,1] op_sel_hi:[0,1] neg_lo:[0,1]
	v_pk_fma_f32 v[18:19], v[16:17], v[22:23], v[18:19] op_sel_hi:[1,0,1]
	s_nop 0
	v_pk_mul_f32 v[22:23], v[20:21], v[18:19] op_sel:[1,1] op_sel_hi:[1,0] neg_lo:[1,0]
	s_nop 0
	v_pk_fma_f32 v[20:21], v[20:21], v[18:19], v[22:23] op_sel_hi:[0,1,1]
	v_pk_mul_f32 v[22:23], v[16:17], v[18:19] op_sel:[1,1] op_sel_hi:[0,1] neg_lo:[0,1]
	v_pk_fma_f32 v[16:17], v[16:17], v[18:19], v[22:23] op_sel_hi:[1,0,1]
	s_nop 0
	v_pk_mul_f32 v[18:19], v[36:37], v[16:17] op_sel:[1,1] op_sel_hi:[1,0] neg_lo:[1,0]
	s_nop 0
	v_pk_fma_f32 v[16:17], v[36:37], v[16:17], v[18:19] op_sel_hi:[0,1,1]
	ds_write2_b64 v13, v[20:21], v[16:17] offset0:224 offset1:240
	v_mov_b32_e32 v16, v1
	v_mov_b32_e32 v10, v178
	v_mov_b32_e32 v17, v177
	s_waitcnt lgkmcnt(0)
	s_barrier
	v_lshlrev_b32_e32 v190, 3, v16
	v_add_u32_e32 v190, 0x1000, v190
	global_load_dwordx2 v[196:197], v190, s[48:49] offset:-4096
	global_load_dwordx2 v[198:199], v190, s[48:49]
	v_add_u32_e32 v190, 0x2000, v190
	global_load_dwordx2 v[200:201], v190, s[48:49] offset:-4096
	global_load_dwordx2 v[202:203], v190, s[48:49]
	v_add_u32_e32 v190, 0x2000, v190
	global_load_dwordx2 v[204:205], v190, s[48:49] offset:-4096
	global_load_dwordx2 v[206:207], v190, s[48:49]
	v_add_u32_e32 v190, 0x2000, v190
	global_load_dwordx2 v[208:209], v190, s[48:49] offset:-4096
	global_load_dwordx2 v[210:211], v190, s[48:49]
	v_add_u32_e32 v190, 0x2000, v190
	global_load_dwordx2 v[212:213], v190, s[48:49] offset:-4096
	global_load_dwordx2 v[214:215], v190, s[48:49]
	v_add_u32_e32 v190, 0x2000, v190
	global_load_dwordx2 v[216:217], v190, s[48:49] offset:-4096
	global_load_dwordx2 v[218:219], v190, s[48:49]
	v_add_u32_e32 v190, 0x2000, v190
	global_load_dwordx2 v[220:221], v190, s[48:49] offset:-4096
	global_load_dwordx2 v[222:223], v190, s[48:49]
	v_add_u32_e32 v190, 0x2000, v190
	global_load_dwordx2 v[224:225], v190, s[48:49] offset:-4096
	global_load_dwordx2 v[226:227], v190, s[48:49]
	v_mov_b32_e32 v50, v166
	v_lshlrev_b32_e32 v13, 3, v17
	v_lshlrev_b32_e32 v48, 3, v10
	v_add3_u32 v10, 0, v13, v48
	v_xor_b32_e32 v13, 1, v17
	v_xor_b32_e32 v34, 8, v17
	v_xor_b32_e32 v36, 9, v17
	v_lshlrev_b32_e32 v13, 3, v13
	v_xor_b32_e32 v15, 2, v17
	v_xor_b32_e32 v24, 3, v17
	v_xor_b32_e32 v26, 4, v17
	v_xor_b32_e32 v28, 5, v17
	v_xor_b32_e32 v30, 6, v17
	v_xor_b32_e32 v32, 7, v17
	v_lshlrev_b32_e32 v34, 3, v34
	v_lshlrev_b32_e32 v36, 3, v36
	v_xor_b32_e32 v38, 10, v17
	v_xor_b32_e32 v40, 11, v17
	v_xor_b32_e32 v42, 12, v17
	v_xor_b32_e32 v44, 13, v17
	v_xor_b32_e32 v46, 14, v17
	v_xor_b32_e32 v17, 15, v17
	v_add3_u32 v13, 0, v13, v48
	v_lshlrev_b32_e32 v15, 3, v15
	v_lshlrev_b32_e32 v24, 3, v24
	v_lshlrev_b32_e32 v26, 3, v26
	v_lshlrev_b32_e32 v28, 3, v28
	v_lshlrev_b32_e32 v30, 3, v30
	v_lshlrev_b32_e32 v32, 3, v32
	v_add3_u32 v57, 0, v34, v48
	v_add3_u32 v58, 0, v36, v48
	v_lshlrev_b32_e32 v38, 3, v38
	v_lshlrev_b32_e32 v40, 3, v40
	v_lshlrev_b32_e32 v42, 3, v42
	v_lshlrev_b32_e32 v44, 3, v44
	v_lshlrev_b32_e32 v46, 3, v46
	v_lshlrev_b32_e32 v17, 3, v17
	ds_read_b64 v[18:19], v10
	ds_read_b64 v[20:21], v13
	v_add3_u32 v15, 0, v15, v48
	v_add3_u32 v52, 0, v24, v48
	v_add3_u32 v53, 0, v26, v48
	v_add3_u32 v54, 0, v28, v48
	v_add3_u32 v55, 0, v30, v48
	v_add3_u32 v56, 0, v32, v48
	ds_read_b64 v[34:35], v57
	ds_read_b64 v[36:37], v58
	v_add3_u32 v59, 0, v38, v48
	v_add3_u32 v60, 0, v40, v48
	v_add3_u32 v61, 0, v42, v48
	v_add3_u32 v62, 0, v44, v48
	v_add3_u32 v63, 0, v46, v48
	v_add3_u32 v64, 0, v17, v48
	ds_read_b64 v[22:23], v15
	ds_read_b64 v[24:25], v52
	ds_read_b64 v[26:27], v53
	ds_read_b64 v[28:29], v54
	ds_read_b64 v[30:31], v55
	ds_read_b64 v[32:33], v56
	ds_read_b64 v[38:39], v59
	ds_read_b64 v[40:41], v60
	ds_read_b64 v[42:43], v61
	ds_read_b64 v[44:45], v62
	ds_read_b64 v[46:47], v63
	ds_read_b64 v[48:49], v64
	s_waitcnt lgkmcnt(13)
	v_pk_add_f32 v[70:71], v[18:19], v[34:35]
	v_pk_add_f32 v[18:19], v[18:19], v[34:35] neg_lo:[0,1] neg_hi:[0,1]
	s_waitcnt lgkmcnt(12)
	v_pk_add_f32 v[34:35], v[20:21], v[36:37]
	v_pk_add_f32 v[20:21], v[20:21], v[36:37] neg_lo:[0,1] neg_hi:[0,1]
	v_mov_b32_e32 v66, v168
	v_mov_b32_e32 v68, v170
	s_nop 0
	v_pk_mul_f32 v[36:37], v[20:21], v[68:69] op_sel:[1,0] op_sel_hi:[0,0] neg_lo:[1,1] neg_hi:[0,1]
	v_pk_fma_f32 v[20:21], v[20:21], v[50:51], v[36:37] op_sel_hi:[1,0,1]
	s_waitcnt lgkmcnt(5)
	v_pk_add_f32 v[36:37], v[22:23], v[38:39]
	v_pk_add_f32 v[22:23], v[22:23], v[38:39] neg_lo:[0,1] neg_hi:[0,1]
	s_nop 0
	v_pk_mul_f32 v[38:39], v[22:23], v[66:67] op_sel:[1,0] op_sel_hi:[0,0] neg_lo:[1,1] neg_hi:[0,1]
	v_pk_fma_f32 v[22:23], v[22:23], v[66:67], v[38:39] op_sel_hi:[1,0,1]
	s_waitcnt lgkmcnt(4)
	v_pk_add_f32 v[38:39], v[24:25], v[40:41]
	v_pk_add_f32 v[24:25], v[24:25], v[40:41] neg_lo:[0,1] neg_hi:[0,1]
	s_nop 0
	v_pk_mul_f32 v[40:41], v[24:25], v[68:69] op_sel_hi:[1,0]
	s_nop 0
	v_pk_fma_f32 v[24:25], v[24:25], v[50:51], v[40:41] op_sel:[1,0,0] op_sel_hi:[0,0,1] neg_lo:[1,1,0] neg_hi:[0,1,0]
	s_waitcnt lgkmcnt(3)
	v_pk_add_f32 v[40:41], v[26:27], v[42:43]
	v_pk_add_f32 v[26:27], v[26:27], v[42:43] neg_lo:[0,1] neg_hi:[0,1]
	v_xor_b32_e32 v73, 0x80000000, v26
	v_mov_b32_e32 v72, v27
	s_waitcnt lgkmcnt(2)
	v_pk_add_f32 v[26:27], v[28:29], v[44:45]
	v_pk_add_f32 v[28:29], v[28:29], v[44:45] neg_lo:[0,1] neg_hi:[0,1]
	s_nop 0
	v_pk_mul_f32 v[42:43], v[28:29], v[68:69] op_sel_hi:[1,0] neg_lo:[0,1] neg_hi:[0,1]
	s_nop 0
	v_pk_fma_f32 v[28:29], v[28:29], v[50:51], v[42:43] op_sel:[1,0,0] op_sel_hi:[0,0,1] neg_lo:[1,1,0] neg_hi:[0,1,0]
	s_waitcnt lgkmcnt(1)
	v_pk_add_f32 v[42:43], v[30:31], v[46:47]
	v_pk_add_f32 v[30:31], v[30:31], v[46:47] neg_lo:[0,1] neg_hi:[0,1]
	s_nop 0
	v_pk_mul_f32 v[44:45], v[30:31], v[66:67] op_sel:[1,0] op_sel_hi:[0,0] neg_lo:[1,1] neg_hi:[0,1]
	s_nop 0
	v_pk_fma_f32 v[30:31], v[30:31], v[66:67], v[44:45] op_sel_hi:[1,0,1] neg_lo:[0,1,0] neg_hi:[0,1,0]
	s_waitcnt lgkmcnt(0)
	v_pk_add_f32 v[44:45], v[32:33], v[48:49]
	v_pk_add_f32 v[32:33], v[32:33], v[48:49] neg_lo:[0,1] neg_hi:[0,1]
	v_pk_add_f32 v[48:49], v[34:35], v[26:27]
	v_pk_add_f32 v[26:27], v[34:35], v[26:27] neg_lo:[0,1] neg_hi:[0,1]
	s_nop 0
	v_pk_mul_f32 v[34:35], v[26:27], v[66:67] op_sel:[1,0] op_sel_hi:[0,0] neg_lo:[1,1] neg_hi:[0,1]
	v_pk_fma_f32 v[26:27], v[26:27], v[66:67], v[34:35] op_sel_hi:[1,0,1]
	v_pk_add_f32 v[34:35], v[36:37], v[42:43]
	v_pk_add_f32 v[36:37], v[36:37], v[42:43] neg_lo:[0,1] neg_hi:[0,1]
	v_pk_mul_f32 v[46:47], v[32:33], v[68:69] op_sel:[1,0] op_sel_hi:[0,0] neg_lo:[1,1] neg_hi:[0,1]
	v_xor_b32_e32 v43, 0x80000000, v36
	v_mov_b32_e32 v42, v37
	v_pk_add_f32 v[36:37], v[38:39], v[44:45]
	v_pk_add_f32 v[38:39], v[38:39], v[44:45] neg_lo:[0,1] neg_hi:[0,1]
	v_pk_fma_f32 v[46:47], v[32:33], v[50:51], v[46:47] op_sel_hi:[1,0,1] neg_lo:[0,1,0] neg_hi:[0,1,0]
	v_pk_add_f32 v[32:33], v[70:71], v[40:41]
	v_pk_mul_f32 v[44:45], v[38:39], v[66:67] op_sel:[1,0] op_sel_hi:[0,0] neg_lo:[1,1] neg_hi:[0,1]
	v_pk_add_f32 v[40:41], v[70:71], v[40:41] neg_lo:[0,1] neg_hi:[0,1]
	v_pk_fma_f32 v[38:39], v[38:39], v[66:67], v[44:45] op_sel_hi:[1,0,1] neg_lo:[0,1,0] neg_hi:[0,1,0]
	v_pk_add_f32 v[44:45], v[32:33], v[34:35]
	v_pk_add_f32 v[32:33], v[32:33], v[34:35] neg_lo:[0,1] neg_hi:[0,1]
	v_pk_add_f32 v[34:35], v[48:49], v[36:37]
	v_pk_add_f32 v[36:37], v[48:49], v[36:37] neg_lo:[0,1] neg_hi:[0,1]
	v_pk_add_f32 v[50:51], v[44:45], v[34:35]
	v_xor_b32_e32 v49, 0x80000000, v36
	v_mov_b32_e32 v48, v37
	v_pk_add_f32 v[36:37], v[44:45], v[34:35] neg_lo:[0,1] neg_hi:[0,1]
	v_pk_add_f32 v[68:69], v[32:33], v[48:49]
	v_pk_add_f32 v[44:45], v[32:33], v[48:49] neg_lo:[0,1] neg_hi:[0,1]
	v_pk_add_f32 v[32:33], v[40:41], v[42:43]
	v_pk_add_f32 v[34:35], v[40:41], v[42:43] neg_lo:[0,1] neg_hi:[0,1]
	v_pk_add_f32 v[40:41], v[26:27], v[38:39]
	v_pk_add_f32 v[26:27], v[26:27], v[38:39] neg_lo:[0,1] neg_hi:[0,1]
	v_pk_add_f32 v[42:43], v[32:33], v[40:41] neg_lo:[0,1] neg_hi:[0,1]
	v_xor_b32_e32 v39, 0x80000000, v26
	v_mov_b32_e32 v38, v27
	v_pk_add_f32 v[26:27], v[32:33], v[40:41]
	v_pk_add_f32 v[40:41], v[20:21], v[28:29]
	v_pk_add_f32 v[20:21], v[20:21], v[28:29] neg_lo:[0,1] neg_hi:[0,1]
	v_pk_add_f32 v[32:33], v[34:35], v[38:39]
	v_pk_mul_f32 v[28:29], v[66:67], v[20:21] op_sel:[0,1] op_sel_hi:[0,0] neg_lo:[1,1] neg_hi:[1,0]
	v_pk_fma_f32 v[20:21], v[66:67], v[20:21], v[28:29] op_sel_hi:[0,1,1]
	v_pk_add_f32 v[28:29], v[22:23], v[30:31]
	v_pk_add_f32 v[22:23], v[22:23], v[30:31] neg_lo:[0,1] neg_hi:[0,1]
	v_pk_add_f32 v[38:39], v[34:35], v[38:39] neg_lo:[0,1] neg_hi:[0,1]
	v_xor_b32_e32 v31, 0x80000000, v22
	v_mov_b32_e32 v30, v23
	v_pk_add_f32 v[22:23], v[24:25], v[46:47]
	v_pk_add_f32 v[24:25], v[24:25], v[46:47] neg_lo:[0,1] neg_hi:[0,1]
	v_pk_add_f32 v[34:35], v[18:19], v[72:73]
	v_pk_mul_f32 v[46:47], v[66:67], v[24:25] op_sel:[0,1] op_sel_hi:[0,0] neg_lo:[1,1] neg_hi:[1,0]
	v_pk_fma_f32 v[24:25], v[66:67], v[24:25], v[46:47] op_sel_hi:[0,1,1] neg_lo:[1,0,0] neg_hi:[1,0,0]
	v_pk_add_f32 v[46:47], v[34:35], v[28:29]
	v_pk_add_f32 v[28:29], v[34:35], v[28:29] neg_lo:[0,1] neg_hi:[0,1]
	v_pk_add_f32 v[34:35], v[40:41], v[22:23]
	v_pk_add_f32 v[22:23], v[40:41], v[22:23] neg_lo:[0,1] neg_hi:[0,1]
	v_pk_add_f32 v[18:19], v[18:19], v[72:73] neg_lo:[0,1] neg_hi:[0,1]
	v_pk_add_f32 v[66:67], v[28:29], v[22:23] op_sel:[0,1] op_sel_hi:[1,0] neg_hi:[0,1]
	v_pk_add_f32 v[48:49], v[28:29], v[22:23] op_sel:[0,1] op_sel_hi:[1,0] neg_lo:[0,1]
	v_pk_add_f32 v[28:29], v[18:19], v[30:31]
	v_pk_add_f32 v[18:19], v[18:19], v[30:31] neg_lo:[0,1] neg_hi:[0,1]
	v_pk_add_f32 v[30:31], v[20:21], v[24:25]
	v_pk_add_f32 v[20:21], v[20:21], v[24:25] neg_lo:[0,1] neg_hi:[0,1]
	v_pk_add_f32 v[22:23], v[46:47], v[34:35]
	v_xor_b32_e32 v25, 0x80000000, v20
	v_mov_b32_e32 v24, v21
	s_waitcnt vmcnt(0)
	v_pk_add_f32 v[40:41], v[46:47], v[34:35] neg_lo:[0,1] neg_hi:[0,1]
	v_pk_add_f32 v[34:35], v[18:19], v[24:25]
	v_pk_add_f32 v[18:19], v[18:19], v[24:25] neg_lo:[0,1] neg_hi:[0,1]
	v_pk_add_f32 v[70:71], v[28:29], v[30:31]
	v_pk_add_f32 v[46:47], v[28:29], v[30:31] neg_lo:[0,1] neg_hi:[0,1]
	s_nop 0
	v_pk_mul_f32 v[24:25], v[50:51], v[196:197] op_sel:[1,1] op_sel_hi:[1,0] neg_lo:[1,0]
	s_nop 0
	v_pk_fma_f32 v[20:21], v[50:51], v[196:197], v[24:25] op_sel_hi:[0,1,1]
	s_nop 0
	v_pk_mul_f32 v[28:29], v[198:199], v[22:23] op_sel:[1,1] op_sel_hi:[0,1] neg_lo:[0,1]
	v_pk_fma_f32 v[22:23], v[198:199], v[22:23], v[28:29] op_sel_hi:[1,0,1]
	s_nop 0
	v_pk_mul_f32 v[28:29], v[26:27], v[200:201] op_sel:[1,1] op_sel_hi:[1,0] neg_lo:[1,0]
	s_nop 0
	v_pk_fma_f32 v[24:25], v[26:27], v[200:201], v[28:29] op_sel_hi:[0,1,1]
	s_nop 0
	v_pk_mul_f32 v[28:29], v[202:203], v[70:71] op_sel:[1,1] op_sel_hi:[0,1] neg_lo:[0,1]
	v_pk_fma_f32 v[26:27], v[202:203], v[70:71], v[28:29] op_sel_hi:[1,0,1]
	s_nop 0
	v_pk_mul_f32 v[30:31], v[68:69], v[204:205] op_sel:[1,1] op_sel_hi:[1,0] neg_lo:[1,0]
	s_nop 0
	v_pk_fma_f32 v[28:29], v[68:69], v[204:205], v[30:31] op_sel_hi:[0,1,1]
	v_mov_b32_e32 v68, v170
	s_nop 0
	v_pk_mul_f32 v[50:51], v[206:207], v[66:67] op_sel:[1,1] op_sel_hi:[0,1] neg_lo:[0,1]
	v_pk_fma_f32 v[30:31], v[206:207], v[66:67], v[50:51] op_sel_hi:[1,0,1]
	s_nop 0
	v_pk_mul_f32 v[66:67], v[32:33], v[208:209] op_sel:[1,1] op_sel_hi:[1,0] neg_lo:[1,0]
	s_nop 0
	v_pk_fma_f32 v[32:33], v[32:33], v[208:209], v[66:67] op_sel_hi:[0,1,1]
	s_nop 0
	v_pk_mul_f32 v[66:67], v[210:211], v[34:35] op_sel:[1,1] op_sel_hi:[0,1] neg_lo:[0,1]
	v_pk_fma_f32 v[34:35], v[210:211], v[34:35], v[66:67] op_sel_hi:[1,0,1]
	s_nop 0
	v_pk_mul_f32 v[66:67], v[36:37], v[212:213] op_sel:[1,1] op_sel_hi:[1,0] neg_lo:[1,0]
	s_nop 0
	v_pk_fma_f32 v[36:37], v[36:37], v[212:213], v[66:67] op_sel_hi:[0,1,1]
	v_pk_add_f32 v[70:71], v[20:21], v[36:37]
	v_pk_add_f32 v[20:21], v[20:21], v[36:37] neg_lo:[0,1] neg_hi:[0,1]
	s_nop 0
	v_pk_mul_f32 v[66:67], v[40:41], v[214:215] op_sel:[1,1] op_sel_hi:[1,0] neg_lo:[1,0]
	s_nop 0
	v_pk_fma_f32 v[40:41], v[40:41], v[214:215], v[66:67] op_sel_hi:[0,1,1]
	v_pk_add_f32 v[36:37], v[22:23], v[40:41]
	v_pk_add_f32 v[22:23], v[22:23], v[40:41] neg_lo:[0,1] neg_hi:[0,1]
	s_nop 0
	v_pk_mul_f32 v[66:67], v[42:43], v[216:217] op_sel:[1,1] op_sel_hi:[1,0] neg_lo:[1,0]
	s_nop 0
	v_pk_fma_f32 v[42:43], v[42:43], v[216:217], v[66:67] op_sel_hi:[0,1,1]
	s_nop 0
	v_pk_mul_f32 v[66:67], v[46:47], v[218:219] op_sel:[1,1] op_sel_hi:[1,0] neg_lo:[1,0]
	s_nop 0
	v_pk_fma_f32 v[46:47], v[46:47], v[218:219], v[66:67] op_sel_hi:[0,1,1]
	s_nop 0
	v_pk_mul_f32 v[66:67], v[44:45], v[220:221] op_sel:[1,1] op_sel_hi:[1,0] neg_lo:[1,0]
	s_nop 0
	v_pk_fma_f32 v[44:45], v[44:45], v[220:221], v[66:67] op_sel_hi:[0,1,1]
	s_nop 0
	v_pk_mul_f32 v[66:67], v[48:49], v[222:223] op_sel:[1,1] op_sel_hi:[1,0] neg_lo:[1,0]
	s_nop 0
	v_pk_fma_f32 v[48:49], v[48:49], v[222:223], v[66:67] op_sel_hi:[0,1,1]
	s_nop 0
	v_pk_mul_f32 v[66:67], v[38:39], v[224:225] op_sel:[1,1] op_sel_hi:[1,0] neg_lo:[1,0]
	s_nop 0
	v_pk_fma_f32 v[38:39], v[38:39], v[224:225], v[66:67] op_sel_hi:[0,1,1]
	v_mov_b32_e32 v50, v226
	v_mov_b32_e32 v51, v227
	v_lshlrev_b32_e32 v190, 3, v16
	v_add_u32_e32 v190, 0x11000, v190
	global_load_dwordx2 v[196:197], v190, s[48:49] offset:-4096
	global_load_dwordx2 v[198:199], v190, s[48:49]
	v_add_u32_e32 v190, 0x2000, v190
	global_load_dwordx2 v[200:201], v190, s[48:49] offset:-4096
	global_load_dwordx2 v[202:203], v190, s[48:49]
	v_add_u32_e32 v190, 0x2000, v190
	global_load_dwordx2 v[204:205], v190, s[48:49] offset:-4096
	global_load_dwordx2 v[206:207], v190, s[48:49]
	v_add_u32_e32 v190, 0x2000, v190
	global_load_dwordx2 v[208:209], v190, s[48:49] offset:-4096
	global_load_dwordx2 v[210:211], v190, s[48:49]
	v_add_u32_e32 v190, 0x2000, v190
	global_load_dwordx2 v[212:213], v190, s[48:49] offset:-4096
	global_load_dwordx2 v[214:215], v190, s[48:49]
	v_add_u32_e32 v190, 0x2000, v190
	global_load_dwordx2 v[216:217], v190, s[48:49] offset:-4096
	global_load_dwordx2 v[218:219], v190, s[48:49]
	v_add_u32_e32 v190, 0x2000, v190
	global_load_dwordx2 v[220:221], v190, s[48:49] offset:-4096
	global_load_dwordx2 v[222:223], v190, s[48:49]
	v_add_u32_e32 v190, 0x2000, v190
	global_load_dwordx2 v[224:225], v190, s[48:49] offset:-4096
	global_load_dwordx2 v[226:227], v190, s[48:49]
	s_nop 0
	v_pk_mul_f32 v[66:67], v[18:19], v[50:51] op_sel:[1,1] op_sel_hi:[1,0] neg_lo:[1,0]
	s_nop 0
	v_pk_fma_f32 v[18:19], v[18:19], v[50:51], v[66:67] op_sel_hi:[0,1,1]
	v_mov_b32_e32 v50, v166
	v_mov_b32_e32 v66, v168
	s_nop 0
	v_pk_mul_f32 v[40:41], v[22:23], v[68:69] op_sel:[1,0] op_sel_hi:[0,0] neg_lo:[1,0]
	v_pk_fma_f32 v[22:23], v[22:23], v[50:51], v[40:41] op_sel_hi:[1,0,1]
	v_pk_add_f32 v[40:41], v[24:25], v[42:43]
	v_pk_add_f32 v[24:25], v[24:25], v[42:43] neg_lo:[0,1] neg_hi:[0,1]
	s_nop 0
	v_pk_mul_f32 v[42:43], v[24:25], v[66:67] op_sel:[1,0] op_sel_hi:[0,0] neg_lo:[1,0]
	v_pk_fma_f32 v[24:25], v[24:25], v[66:67], v[42:43] op_sel_hi:[1,0,1]
	v_pk_add_f32 v[42:43], v[26:27], v[46:47]
	v_pk_add_f32 v[26:27], v[26:27], v[46:47] neg_lo:[0,1] neg_hi:[0,1]
	s_nop 0
	v_pk_mul_f32 v[46:47], v[26:27], v[68:69] op_sel_hi:[1,0]
	s_nop 0
	v_pk_fma_f32 v[26:27], v[26:27], v[50:51], v[46:47] op_sel:[1,0,0] op_sel_hi:[0,0,1] neg_lo:[1,0,0]
	v_pk_add_f32 v[46:47], v[28:29], v[44:45]
	v_pk_add_f32 v[28:29], v[28:29], v[44:45] neg_lo:[0,1] neg_hi:[0,1]
	v_mov_b32_e32 v17, v177
	v_xor_b32_e32 v44, 0x80000000, v29
	v_mov_b32_e32 v45, v28
	v_pk_add_f32 v[28:29], v[30:31], v[48:49]
	v_pk_add_f32 v[30:31], v[30:31], v[48:49] neg_lo:[0,1] neg_hi:[0,1]
	s_nop 0
	v_pk_mul_f32 v[48:49], v[30:31], v[68:69] op_sel_hi:[1,0] neg_lo:[0,1] neg_hi:[0,1]
	s_nop 0
	v_pk_fma_f32 v[30:31], v[30:31], v[50:51], v[48:49] op_sel:[1,0,0] op_sel_hi:[0,0,1] neg_lo:[1,0,0]
	v_pk_add_f32 v[48:49], v[32:33], v[38:39]
	v_pk_add_f32 v[32:33], v[32:33], v[38:39] neg_lo:[0,1] neg_hi:[0,1]
	s_nop 0
	v_pk_mul_f32 v[38:39], v[32:33], v[66:67] op_sel:[1,0] op_sel_hi:[0,0] neg_lo:[1,0]
	s_nop 0
	v_pk_fma_f32 v[32:33], v[32:33], v[66:67], v[38:39] op_sel_hi:[1,0,1] neg_lo:[0,1,0] neg_hi:[0,1,0]
	v_pk_add_f32 v[38:39], v[34:35], v[18:19]
	v_pk_add_f32 v[18:19], v[34:35], v[18:19] neg_lo:[0,1] neg_hi:[0,1]
	s_nop 0
	v_pk_mul_f32 v[34:35], v[18:19], v[68:69] op_sel:[1,0] op_sel_hi:[0,0] neg_lo:[1,0]
	v_mov_b32_e32 v68, v170
	v_pk_fma_f32 v[18:19], v[18:19], v[50:51], v[34:35] op_sel_hi:[1,0,1] neg_lo:[0,1,0] neg_hi:[0,1,0]
	v_pk_add_f32 v[50:51], v[36:37], v[28:29]
	v_pk_add_f32 v[28:29], v[36:37], v[28:29] neg_lo:[0,1] neg_hi:[0,1]
	v_pk_add_f32 v[34:35], v[70:71], v[46:47]
	v_pk_mul_f32 v[36:37], v[28:29], v[66:67] op_sel:[1,0] op_sel_hi:[0,0] neg_lo:[1,0]
	v_pk_add_f32 v[46:47], v[70:71], v[46:47] neg_lo:[0,1] neg_hi:[0,1]
	v_pk_fma_f32 v[28:29], v[28:29], v[66:67], v[36:37] op_sel_hi:[1,0,1]
	v_pk_add_f32 v[36:37], v[40:41], v[48:49]
	v_pk_add_f32 v[40:41], v[40:41], v[48:49] neg_lo:[0,1] neg_hi:[0,1]
	s_nop 0
	v_xor_b32_e32 v48, 0x80000000, v41
	v_mov_b32_e32 v49, v40
	v_pk_add_f32 v[40:41], v[42:43], v[38:39]
	v_pk_add_f32 v[38:39], v[42:43], v[38:39] neg_lo:[0,1] neg_hi:[0,1]
	s_nop 0
	v_pk_mul_f32 v[42:43], v[66:67], v[38:39] op_sel:[0,1] op_sel_hi:[0,0] neg_lo:[0,1]
	v_pk_fma_f32 v[38:39], v[38:39], v[66:67], v[42:43] op_sel_hi:[1,0,1] neg_lo:[0,1,0] neg_hi:[0,1,0]
	v_pk_add_f32 v[42:43], v[34:35], v[36:37]
	v_pk_add_f32 v[34:35], v[34:35], v[36:37] neg_lo:[0,1] neg_hi:[0,1]
	v_pk_add_f32 v[36:37], v[50:51], v[40:41]
	v_pk_add_f32 v[40:41], v[50:51], v[40:41] neg_lo:[0,1] neg_hi:[0,1]
	s_nop 0
	v_xor_b32_e32 v50, 0x80000000, v41
	v_mov_b32_e32 v51, v40
	v_pk_add_f32 v[40:41], v[42:43], v[36:37]
	v_pk_add_f32 v[36:37], v[42:43], v[36:37] neg_lo:[0,1] neg_hi:[0,1]
	v_pk_add_f32 v[42:43], v[34:35], v[50:51]
	v_pk_add_f32 v[34:35], v[34:35], v[50:51] neg_lo:[0,1] neg_hi:[0,1]
	v_pk_add_f32 v[50:51], v[46:47], v[48:49]
	v_pk_add_f32 v[46:47], v[46:47], v[48:49] neg_lo:[0,1] neg_hi:[0,1]
	v_pk_add_f32 v[48:49], v[28:29], v[38:39]
	v_pk_add_f32 v[28:29], v[28:29], v[38:39] neg_lo:[0,1] neg_hi:[0,1]
	s_nop 0
	v_xor_b32_e32 v38, 0x80000000, v29
	v_mov_b32_e32 v39, v28
	v_pk_add_f32 v[28:29], v[50:51], v[48:49]
	v_pk_add_f32 v[48:49], v[50:51], v[48:49] neg_lo:[0,1] neg_hi:[0,1]
	v_pk_add_f32 v[50:51], v[46:47], v[38:39]
	v_pk_add_f32 v[38:39], v[46:47], v[38:39] neg_lo:[0,1] neg_hi:[0,1]
	v_pk_add_f32 v[46:47], v[20:21], v[44:45]
	v_pk_add_f32 v[20:21], v[20:21], v[44:45] neg_lo:[0,1] neg_hi:[0,1]
	v_pk_add_f32 v[44:45], v[22:23], v[30:31]
	v_pk_add_f32 v[22:23], v[22:23], v[30:31] neg_lo:[0,1] neg_hi:[0,1]
	s_nop 0
	v_pk_mul_f32 v[30:31], v[66:67], v[22:23] op_sel:[0,1] op_sel_hi:[0,0] neg_lo:[0,1]
	v_pk_fma_f32 v[22:23], v[66:67], v[22:23], v[30:31] op_sel_hi:[0,1,1]
	v_pk_add_f32 v[30:31], v[24:25], v[32:33]
	v_pk_add_f32 v[24:25], v[24:25], v[32:33] neg_lo:[0,1] neg_hi:[0,1]
	s_nop 0
	v_xor_b32_e32 v32, 0x80000000, v25
	v_mov_b32_e32 v33, v24
	v_pk_add_f32 v[24:25], v[26:27], v[18:19]
	v_pk_add_f32 v[18:19], v[26:27], v[18:19] neg_lo:[0,1] neg_hi:[0,1]
	s_nop 0
	v_pk_mul_f32 v[26:27], v[66:67], v[18:19] op_sel:[0,1] op_sel_hi:[0,0] neg_lo:[0,1]
	v_pk_fma_f32 v[18:19], v[66:67], v[18:19], v[26:27] op_sel_hi:[0,1,1] neg_lo:[1,0,0] neg_hi:[1,0,0]
	v_pk_add_f32 v[26:27], v[46:47], v[30:31]
	v_pk_add_f32 v[30:31], v[46:47], v[30:31] neg_lo:[0,1] neg_hi:[0,1]
	v_pk_add_f32 v[46:47], v[44:45], v[24:25]
	v_pk_add_f32 v[24:25], v[44:45], v[24:25] neg_lo:[0,1] neg_hi:[0,1]
	v_mov_b32_e32 v66, v168
	v_xor_b32_e32 v44, 0x80000000, v25
	v_mov_b32_e32 v45, v24
	v_pk_add_f32 v[24:25], v[26:27], v[46:47]
	v_pk_add_f32 v[26:27], v[26:27], v[46:47] neg_lo:[0,1] neg_hi:[0,1]
	v_pk_add_f32 v[46:47], v[30:31], v[44:45]
	v_pk_add_f32 v[30:31], v[30:31], v[44:45] neg_lo:[0,1] neg_hi:[0,1]
	v_pk_add_f32 v[44:45], v[20:21], v[32:33]
	v_pk_add_f32 v[20:21], v[20:21], v[32:33] neg_lo:[0,1] neg_hi:[0,1]
	v_pk_add_f32 v[32:33], v[22:23], v[18:19]
	v_pk_add_f32 v[18:19], v[22:23], v[18:19] neg_lo:[0,1] neg_hi:[0,1]
	s_nop 0
	v_xor_b32_e32 v22, 0x80000000, v19
	v_mov_b32_e32 v23, v18
	v_pk_add_f32 v[18:19], v[44:45], v[32:33]
	v_pk_add_f32 v[32:33], v[44:45], v[32:33] neg_lo:[0,1] neg_hi:[0,1]
	v_pk_add_f32 v[44:45], v[20:21], v[22:23]
	v_pk_add_f32 v[20:21], v[20:21], v[22:23] neg_lo:[0,1] neg_hi:[0,1]
	ds_write_b64 v10, v[40:41]
	ds_write_b64 v13, v[24:25]
	ds_write_b64 v15, v[28:29]
	ds_write_b64 v52, v[18:19]
	ds_write_b64 v53, v[42:43]
	ds_write_b64 v54, v[46:47]
	ds_write_b64 v55, v[50:51]
	ds_write_b64 v56, v[44:45]
	ds_write_b64 v57, v[36:37]
	ds_write_b64 v58, v[26:27]
	ds_write_b64 v59, v[48:49]
	ds_write_b64 v60, v[32:33]
	ds_write_b64 v61, v[34:35]
	ds_write_b64 v62, v[30:31]
	ds_write_b64 v63, v[38:39]
	ds_write_b64 v64, v[20:21]
	v_mov_b32_e32 v10, v179
	v_mov_b32_e32 v64, v166
	v_lshlrev_b32_e32 v13, 3, v17
	v_lshlrev_b32_e32 v48, 3, v10
	v_add3_u32 v10, 0, v13, v48
	v_xor_b32_e32 v13, 1, v17
	v_xor_b32_e32 v34, 8, v17
	v_xor_b32_e32 v36, 9, v17
	v_lshlrev_b32_e32 v13, 3, v13
	v_xor_b32_e32 v15, 2, v17
	v_xor_b32_e32 v24, 3, v17
	v_xor_b32_e32 v26, 4, v17
	v_xor_b32_e32 v28, 5, v17
	v_xor_b32_e32 v30, 6, v17
	v_xor_b32_e32 v32, 7, v17
	v_lshlrev_b32_e32 v34, 3, v34
	v_lshlrev_b32_e32 v36, 3, v36
	v_xor_b32_e32 v38, 10, v17
	v_xor_b32_e32 v40, 11, v17
	v_xor_b32_e32 v42, 12, v17
	v_xor_b32_e32 v44, 13, v17
	v_xor_b32_e32 v46, 14, v17
	v_xor_b32_e32 v17, 15, v17
	v_add3_u32 v13, 0, v13, v48
	v_lshlrev_b32_e32 v15, 3, v15
	v_lshlrev_b32_e32 v24, 3, v24
	v_lshlrev_b32_e32 v26, 3, v26
	v_lshlrev_b32_e32 v28, 3, v28
	v_lshlrev_b32_e32 v30, 3, v30
	v_lshlrev_b32_e32 v32, 3, v32
	v_add3_u32 v55, 0, v34, v48
	v_add3_u32 v56, 0, v36, v48
	v_lshlrev_b32_e32 v38, 3, v38
	v_lshlrev_b32_e32 v40, 3, v40
	v_lshlrev_b32_e32 v42, 3, v42
	v_lshlrev_b32_e32 v44, 3, v44
	v_lshlrev_b32_e32 v46, 3, v46
	v_lshlrev_b32_e32 v17, 3, v17
	ds_read_b64 v[18:19], v10
	ds_read_b64 v[20:21], v13
	v_add3_u32 v15, 0, v15, v48
	v_add3_u32 v50, 0, v24, v48
	v_add3_u32 v51, 0, v26, v48
	v_add3_u32 v52, 0, v28, v48
	v_add3_u32 v53, 0, v30, v48
	v_add3_u32 v54, 0, v32, v48
	ds_read_b64 v[34:35], v55
	ds_read_b64 v[36:37], v56
	v_add3_u32 v57, 0, v38, v48
	v_add3_u32 v58, 0, v40, v48
	v_add3_u32 v59, 0, v42, v48
	v_add3_u32 v60, 0, v44, v48
	v_add3_u32 v61, 0, v46, v48
	v_add3_u32 v62, 0, v17, v48
	ds_read_b64 v[22:23], v15
	ds_read_b64 v[24:25], v50
	ds_read_b64 v[26:27], v51
	ds_read_b64 v[28:29], v52
	ds_read_b64 v[30:31], v53
	ds_read_b64 v[32:33], v54
	ds_read_b64 v[38:39], v57
	ds_read_b64 v[40:41], v58
	ds_read_b64 v[42:43], v59
	ds_read_b64 v[44:45], v60
	ds_read_b64 v[46:47], v61
	ds_read_b64 v[48:49], v62
	s_waitcnt lgkmcnt(13)
	v_pk_add_f32 v[70:71], v[18:19], v[34:35]
	v_pk_add_f32 v[18:19], v[18:19], v[34:35] neg_lo:[0,1] neg_hi:[0,1]
	s_waitcnt lgkmcnt(12)
	v_pk_add_f32 v[34:35], v[20:21], v[36:37]
	v_pk_add_f32 v[20:21], v[20:21], v[36:37] neg_lo:[0,1] neg_hi:[0,1]
	s_nop 0
	v_pk_mul_f32 v[36:37], v[20:21], v[68:69] op_sel:[1,0] op_sel_hi:[0,0] neg_lo:[1,1] neg_hi:[0,1]
	v_pk_fma_f32 v[20:21], v[20:21], v[64:65], v[36:37] op_sel_hi:[1,0,1]
	s_waitcnt lgkmcnt(5)
	v_pk_add_f32 v[36:37], v[22:23], v[38:39]
	v_pk_add_f32 v[22:23], v[22:23], v[38:39] neg_lo:[0,1] neg_hi:[0,1]
	s_nop 0
	v_pk_mul_f32 v[38:39], v[22:23], v[66:67] op_sel:[1,0] op_sel_hi:[0,0] neg_lo:[1,1] neg_hi:[0,1]
	v_pk_fma_f32 v[22:23], v[22:23], v[66:67], v[38:39] op_sel_hi:[1,0,1]
	s_waitcnt lgkmcnt(4)
	v_pk_add_f32 v[38:39], v[24:25], v[40:41]
	v_pk_add_f32 v[24:25], v[24:25], v[40:41] neg_lo:[0,1] neg_hi:[0,1]
	s_nop 0
	v_pk_mul_f32 v[40:41], v[24:25], v[68:69] op_sel_hi:[1,0]
	s_nop 0
	v_pk_fma_f32 v[24:25], v[24:25], v[64:65], v[40:41] op_sel:[1,0,0] op_sel_hi:[0,0,1] neg_lo:[1,1,0] neg_hi:[0,1,0]
	s_waitcnt lgkmcnt(3)
	v_pk_add_f32 v[40:41], v[26:27], v[42:43]
	v_pk_add_f32 v[26:27], v[26:27], v[42:43] neg_lo:[0,1] neg_hi:[0,1]
	s_nop 0
	v_xor_b32_e32 v73, 0x80000000, v26
	v_mov_b32_e32 v72, v27
	s_waitcnt lgkmcnt(2)
	v_pk_add_f32 v[26:27], v[28:29], v[44:45]
	v_pk_add_f32 v[28:29], v[28:29], v[44:45] neg_lo:[0,1] neg_hi:[0,1]
	s_nop 0
	v_pk_mul_f32 v[42:43], v[28:29], v[68:69] op_sel_hi:[1,0] neg_lo:[0,1] neg_hi:[0,1]
	s_nop 0
	v_pk_fma_f32 v[28:29], v[28:29], v[64:65], v[42:43] op_sel:[1,0,0] op_sel_hi:[0,0,1] neg_lo:[1,1,0] neg_hi:[0,1,0]
	s_waitcnt lgkmcnt(1)
	v_pk_add_f32 v[42:43], v[30:31], v[46:47]
	v_pk_add_f32 v[30:31], v[30:31], v[46:47] neg_lo:[0,1] neg_hi:[0,1]
	s_nop 0
	v_pk_mul_f32 v[44:45], v[30:31], v[66:67] op_sel:[1,0] op_sel_hi:[0,0] neg_lo:[1,1] neg_hi:[0,1]
	s_nop 0
	v_pk_fma_f32 v[30:31], v[30:31], v[66:67], v[44:45] op_sel_hi:[1,0,1] neg_lo:[0,1,0] neg_hi:[0,1,0]
	s_waitcnt lgkmcnt(0)
	v_pk_add_f32 v[44:45], v[32:33], v[48:49]
	v_pk_add_f32 v[32:33], v[32:33], v[48:49] neg_lo:[0,1] neg_hi:[0,1]
	v_pk_add_f32 v[48:49], v[34:35], v[26:27]
	v_pk_add_f32 v[26:27], v[34:35], v[26:27] neg_lo:[0,1] neg_hi:[0,1]
	s_nop 0
	v_pk_mul_f32 v[34:35], v[26:27], v[66:67] op_sel:[1,0] op_sel_hi:[0,0] neg_lo:[1,1] neg_hi:[0,1]
	v_pk_fma_f32 v[26:27], v[26:27], v[66:67], v[34:35] op_sel_hi:[1,0,1]
	v_pk_add_f32 v[34:35], v[36:37], v[42:43]
	v_pk_add_f32 v[36:37], v[36:37], v[42:43] neg_lo:[0,1] neg_hi:[0,1]
	v_pk_mul_f32 v[46:47], v[32:33], v[68:69] op_sel:[1,0] op_sel_hi:[0,0] neg_lo:[1,1] neg_hi:[0,1]
	v_xor_b32_e32 v43, 0x80000000, v36
	v_mov_b32_e32 v42, v37
	v_pk_add_f32 v[36:37], v[38:39], v[44:45]
	v_pk_add_f32 v[38:39], v[38:39], v[44:45] neg_lo:[0,1] neg_hi:[0,1]
	v_pk_fma_f32 v[46:47], v[32:33], v[64:65], v[46:47] op_sel_hi:[1,0,1] neg_lo:[0,1,0] neg_hi:[0,1,0]
	v_pk_add_f32 v[32:33], v[70:71], v[40:41]
	v_pk_mul_f32 v[44:45], v[38:39], v[66:67] op_sel:[1,0] op_sel_hi:[0,0] neg_lo:[1,1] neg_hi:[0,1]
	v_pk_add_f32 v[40:41], v[70:71], v[40:41] neg_lo:[0,1] neg_hi:[0,1]
	v_pk_fma_f32 v[38:39], v[38:39], v[66:67], v[44:45] op_sel_hi:[1,0,1] neg_lo:[0,1,0] neg_hi:[0,1,0]
	v_pk_add_f32 v[44:45], v[32:33], v[34:35]
	v_pk_add_f32 v[32:33], v[32:33], v[34:35] neg_lo:[0,1] neg_hi:[0,1]
	v_pk_add_f32 v[34:35], v[48:49], v[36:37]
	v_pk_add_f32 v[36:37], v[48:49], v[36:37] neg_lo:[0,1] neg_hi:[0,1]
	v_pk_add_f32 v[64:65], v[44:45], v[34:35]
	v_xor_b32_e32 v49, 0x80000000, v36
	v_mov_b32_e32 v48, v37
	v_pk_add_f32 v[36:37], v[44:45], v[34:35] neg_lo:[0,1] neg_hi:[0,1]
	v_pk_add_f32 v[68:69], v[32:33], v[48:49]
	v_pk_add_f32 v[44:45], v[32:33], v[48:49] neg_lo:[0,1] neg_hi:[0,1]
	v_pk_add_f32 v[32:33], v[40:41], v[42:43]
	v_pk_add_f32 v[34:35], v[40:41], v[42:43] neg_lo:[0,1] neg_hi:[0,1]
	v_pk_add_f32 v[40:41], v[26:27], v[38:39]
	v_pk_add_f32 v[26:27], v[26:27], v[38:39] neg_lo:[0,1] neg_hi:[0,1]
	v_pk_add_f32 v[42:43], v[32:33], v[40:41] neg_lo:[0,1] neg_hi:[0,1]
	v_xor_b32_e32 v39, 0x80000000, v26
	v_mov_b32_e32 v38, v27
	v_pk_add_f32 v[26:27], v[32:33], v[40:41]
	v_pk_add_f32 v[40:41], v[20:21], v[28:29]
	v_pk_add_f32 v[20:21], v[20:21], v[28:29] neg_lo:[0,1] neg_hi:[0,1]
	v_pk_add_f32 v[32:33], v[34:35], v[38:39]
	v_pk_mul_f32 v[28:29], v[66:67], v[20:21] op_sel:[0,1] op_sel_hi:[0,0] neg_lo:[1,1] neg_hi:[1,0]
	v_pk_fma_f32 v[20:21], v[66:67], v[20:21], v[28:29] op_sel_hi:[0,1,1]
	v_pk_add_f32 v[28:29], v[22:23], v[30:31]
	v_pk_add_f32 v[22:23], v[22:23], v[30:31] neg_lo:[0,1] neg_hi:[0,1]
	v_pk_add_f32 v[38:39], v[34:35], v[38:39] neg_lo:[0,1] neg_hi:[0,1]
	v_xor_b32_e32 v31, 0x80000000, v22
	v_mov_b32_e32 v30, v23
	v_pk_add_f32 v[22:23], v[24:25], v[46:47]
	v_pk_add_f32 v[24:25], v[24:25], v[46:47] neg_lo:[0,1] neg_hi:[0,1]
	v_pk_add_f32 v[34:35], v[18:19], v[72:73]
	v_pk_mul_f32 v[46:47], v[66:67], v[24:25] op_sel:[0,1] op_sel_hi:[0,0] neg_lo:[1,1] neg_hi:[1,0]
	v_pk_fma_f32 v[24:25], v[66:67], v[24:25], v[46:47] op_sel_hi:[0,1,1] neg_lo:[1,0,0] neg_hi:[1,0,0]
	v_pk_add_f32 v[46:47], v[34:35], v[28:29]
	v_pk_add_f32 v[28:29], v[34:35], v[28:29] neg_lo:[0,1] neg_hi:[0,1]
	v_pk_add_f32 v[34:35], v[40:41], v[22:23]
	v_pk_add_f32 v[22:23], v[40:41], v[22:23] neg_lo:[0,1] neg_hi:[0,1]
	v_pk_add_f32 v[18:19], v[18:19], v[72:73] neg_lo:[0,1] neg_hi:[0,1]
	v_pk_add_f32 v[66:67], v[28:29], v[22:23] op_sel:[0,1] op_sel_hi:[1,0] neg_hi:[0,1]
	v_pk_add_f32 v[48:49], v[28:29], v[22:23] op_sel:[0,1] op_sel_hi:[1,0] neg_lo:[0,1]
	v_pk_add_f32 v[28:29], v[18:19], v[30:31]
	v_pk_add_f32 v[18:19], v[18:19], v[30:31] neg_lo:[0,1] neg_hi:[0,1]
	v_pk_add_f32 v[30:31], v[20:21], v[24:25]
	v_pk_add_f32 v[20:21], v[20:21], v[24:25] neg_lo:[0,1] neg_hi:[0,1]
	v_pk_add_f32 v[22:23], v[46:47], v[34:35]
	v_xor_b32_e32 v25, 0x80000000, v20
	v_mov_b32_e32 v24, v21
	s_waitcnt vmcnt(0)
	v_pk_add_f32 v[40:41], v[46:47], v[34:35] neg_lo:[0,1] neg_hi:[0,1]
	v_pk_add_f32 v[34:35], v[18:19], v[24:25]
	v_pk_add_f32 v[18:19], v[18:19], v[24:25] neg_lo:[0,1] neg_hi:[0,1]
	v_pk_add_f32 v[70:71], v[28:29], v[30:31]
	v_pk_add_f32 v[46:47], v[28:29], v[30:31] neg_lo:[0,1] neg_hi:[0,1]
	s_nop 0
	v_pk_mul_f32 v[24:25], v[64:65], v[196:197] op_sel:[1,1] op_sel_hi:[1,0] neg_lo:[1,0]
	s_nop 0
	v_pk_fma_f32 v[20:21], v[64:65], v[196:197], v[24:25] op_sel_hi:[0,1,1]
	s_nop 0
	v_pk_mul_f32 v[28:29], v[198:199], v[22:23] op_sel:[1,1] op_sel_hi:[0,1] neg_lo:[0,1]
	v_pk_fma_f32 v[22:23], v[198:199], v[22:23], v[28:29] op_sel_hi:[1,0,1]
	s_nop 0
	v_pk_mul_f32 v[28:29], v[26:27], v[200:201] op_sel:[1,1] op_sel_hi:[1,0] neg_lo:[1,0]
	s_nop 0
	v_pk_fma_f32 v[24:25], v[26:27], v[200:201], v[28:29] op_sel_hi:[0,1,1]
	s_nop 0
	v_pk_mul_f32 v[28:29], v[202:203], v[70:71] op_sel:[1,1] op_sel_hi:[0,1] neg_lo:[0,1]
	v_pk_fma_f32 v[26:27], v[202:203], v[70:71], v[28:29] op_sel_hi:[1,0,1]
	s_nop 0
	v_pk_mul_f32 v[30:31], v[68:69], v[204:205] op_sel:[1,1] op_sel_hi:[1,0] neg_lo:[1,0]
	s_nop 0
	v_pk_fma_f32 v[28:29], v[68:69], v[204:205], v[30:31] op_sel_hi:[0,1,1]
	s_nop 0
	v_pk_mul_f32 v[64:65], v[206:207], v[66:67] op_sel:[1,1] op_sel_hi:[0,1] neg_lo:[0,1]
	v_pk_fma_f32 v[30:31], v[206:207], v[66:67], v[64:65] op_sel_hi:[1,0,1]
	s_nop 0
	v_pk_mul_f32 v[66:67], v[32:33], v[208:209] op_sel:[1,1] op_sel_hi:[1,0] neg_lo:[1,0]
	s_nop 0
	v_pk_fma_f32 v[32:33], v[32:33], v[208:209], v[66:67] op_sel_hi:[0,1,1]
	s_nop 0
	v_pk_mul_f32 v[66:67], v[210:211], v[34:35] op_sel:[1,1] op_sel_hi:[0,1] neg_lo:[0,1]
	v_pk_fma_f32 v[34:35], v[210:211], v[34:35], v[66:67] op_sel_hi:[1,0,1]
	s_nop 0
	v_pk_mul_f32 v[66:67], v[36:37], v[212:213] op_sel:[1,1] op_sel_hi:[1,0] neg_lo:[1,0]
	s_nop 0
	v_pk_fma_f32 v[36:37], v[36:37], v[212:213], v[66:67] op_sel_hi:[0,1,1]
	v_pk_add_f32 v[68:69], v[20:21], v[36:37]
	v_pk_add_f32 v[20:21], v[20:21], v[36:37] neg_lo:[0,1] neg_hi:[0,1]
	s_nop 0
	v_pk_mul_f32 v[66:67], v[40:41], v[214:215] op_sel:[1,1] op_sel_hi:[1,0] neg_lo:[1,0]
	s_nop 0
	v_pk_fma_f32 v[40:41], v[40:41], v[214:215], v[66:67] op_sel_hi:[0,1,1]
	v_pk_add_f32 v[36:37], v[22:23], v[40:41]
	v_pk_add_f32 v[22:23], v[22:23], v[40:41] neg_lo:[0,1] neg_hi:[0,1]
	s_nop 0
	v_pk_mul_f32 v[66:67], v[42:43], v[216:217] op_sel:[1,1] op_sel_hi:[1,0] neg_lo:[1,0]
	s_nop 0
	v_pk_fma_f32 v[42:43], v[42:43], v[216:217], v[66:67] op_sel_hi:[0,1,1]
	s_nop 0
	v_pk_mul_f32 v[66:67], v[46:47], v[218:219] op_sel:[1,1] op_sel_hi:[1,0] neg_lo:[1,0]
	s_nop 0
	v_pk_fma_f32 v[46:47], v[46:47], v[218:219], v[66:67] op_sel_hi:[0,1,1]
	s_nop 0
	v_pk_mul_f32 v[66:67], v[44:45], v[220:221] op_sel:[1,1] op_sel_hi:[1,0] neg_lo:[1,0]
	s_nop 0
	v_pk_fma_f32 v[44:45], v[44:45], v[220:221], v[66:67] op_sel_hi:[0,1,1]
	s_nop 0
	v_pk_mul_f32 v[66:67], v[48:49], v[222:223] op_sel:[1,1] op_sel_hi:[1,0] neg_lo:[1,0]
	s_nop 0
	v_pk_fma_f32 v[48:49], v[48:49], v[222:223], v[66:67] op_sel_hi:[0,1,1]
	s_nop 0
	v_pk_mul_f32 v[66:67], v[38:39], v[224:225] op_sel:[1,1] op_sel_hi:[1,0] neg_lo:[1,0]
	s_nop 0
	v_pk_fma_f32 v[38:39], v[38:39], v[224:225], v[66:67] op_sel_hi:[0,1,1]
	s_nop 0
	v_pk_mul_f32 v[64:65], v[18:19], v[226:227] op_sel:[1,1] op_sel_hi:[1,0] neg_lo:[1,0]
	v_mov_b32_e32 v66, v170
	v_pk_fma_f32 v[16:17], v[18:19], v[226:227], v[64:65] op_sel_hi:[0,1,1]
	v_mov_b32_e32 v64, v168
	v_mov_b32_e32 v18, v166
	s_nop 0
	s_nop 0
	v_pk_mul_f32 v[40:41], v[22:23], v[66:67] op_sel:[1,0] op_sel_hi:[0,0] neg_lo:[1,0]
	v_mov_b32_e32 v19, v172
	s_nop 0
	v_pk_fma_f32 v[22:23], v[22:23], v[18:19], v[40:41] op_sel_hi:[1,0,1]
	v_pk_add_f32 v[40:41], v[24:25], v[42:43]
	v_pk_add_f32 v[24:25], v[24:25], v[42:43] neg_lo:[0,1] neg_hi:[0,1]
	s_nop 0
	v_pk_mul_f32 v[42:43], v[24:25], v[64:65] op_sel:[1,0] op_sel_hi:[0,0] neg_lo:[1,0]
	s_nop 0
	v_pk_fma_f32 v[24:25], v[24:25], v[64:65], v[42:43] op_sel_hi:[1,0,1]
	v_pk_add_f32 v[42:43], v[26:27], v[46:47]
	v_pk_add_f32 v[26:27], v[26:27], v[46:47] neg_lo:[0,1] neg_hi:[0,1]
	s_nop 0
	v_pk_mul_f32 v[46:47], v[26:27], v[66:67] op_sel_hi:[1,0]
	s_nop 0
	v_pk_fma_f32 v[26:27], v[26:27], v[18:19], v[46:47] op_sel:[1,0,0] op_sel_hi:[0,0,1] neg_lo:[1,0,0]
	v_pk_add_f32 v[46:47], v[28:29], v[44:45]
	v_pk_add_f32 v[28:29], v[28:29], v[44:45] neg_lo:[0,1] neg_hi:[0,1]
	s_nop 0
	v_xor_b32_e32 v44, 0x80000000, v29
	v_mov_b32_e32 v45, v28
	v_pk_add_f32 v[28:29], v[30:31], v[48:49]
	v_pk_add_f32 v[30:31], v[30:31], v[48:49] neg_lo:[0,1] neg_hi:[0,1]
	s_nop 0
	v_pk_mul_f32 v[48:49], v[30:31], v[66:67] op_sel_hi:[1,0] neg_lo:[0,1] neg_hi:[0,1]
	s_nop 0
	v_pk_fma_f32 v[30:31], v[30:31], v[18:19], v[48:49] op_sel:[1,0,0] op_sel_hi:[0,0,1] neg_lo:[1,0,0]
	v_pk_add_f32 v[48:49], v[32:33], v[38:39]
	v_pk_add_f32 v[32:33], v[32:33], v[38:39] neg_lo:[0,1] neg_hi:[0,1]
	s_nop 0
	v_pk_mul_f32 v[38:39], v[32:33], v[64:65] op_sel:[1,0] op_sel_hi:[0,0] neg_lo:[1,0]
	s_nop 0
	v_pk_fma_f32 v[32:33], v[32:33], v[64:65], v[38:39] op_sel_hi:[1,0,1] neg_lo:[0,1,0] neg_hi:[0,1,0]
	v_pk_add_f32 v[38:39], v[34:35], v[16:17]
	v_pk_add_f32 v[16:17], v[34:35], v[16:17] neg_lo:[0,1] neg_hi:[0,1]
	s_nop 0
	v_pk_mul_f32 v[34:35], v[16:17], v[66:67] op_sel:[1,0] op_sel_hi:[0,0] neg_lo:[1,0]
	s_nop 0
	v_pk_fma_f32 v[16:17], v[16:17], v[18:19], v[34:35] op_sel_hi:[1,0,1] neg_lo:[0,1,0] neg_hi:[0,1,0]
	v_pk_add_f32 v[18:19], v[68:69], v[46:47]
	v_pk_add_f32 v[34:35], v[68:69], v[46:47] neg_lo:[0,1] neg_hi:[0,1]
	v_pk_add_f32 v[46:47], v[36:37], v[28:29]
	v_pk_add_f32 v[28:29], v[36:37], v[28:29] neg_lo:[0,1] neg_hi:[0,1]
	s_nop 0
	v_pk_mul_f32 v[36:37], v[28:29], v[64:65] op_sel:[1,0] op_sel_hi:[0,0] neg_lo:[1,0]
	s_nop 0
	v_pk_fma_f32 v[28:29], v[28:29], v[64:65], v[36:37] op_sel_hi:[1,0,1]
	v_pk_add_f32 v[36:37], v[40:41], v[48:49]
	v_pk_add_f32 v[40:41], v[40:41], v[48:49] neg_lo:[0,1] neg_hi:[0,1]
	s_nop 0
	v_xor_b32_e32 v48, 0x80000000, v41
	v_mov_b32_e32 v49, v40
	v_pk_add_f32 v[40:41], v[42:43], v[38:39]
	v_pk_add_f32 v[38:39], v[42:43], v[38:39] neg_lo:[0,1] neg_hi:[0,1]
	s_nop 0
	v_pk_mul_f32 v[42:43], v[64:65], v[38:39] op_sel:[0,1] op_sel_hi:[0,0] neg_lo:[0,1]
	v_pk_fma_f32 v[38:39], v[38:39], v[64:65], v[42:43] op_sel_hi:[1,0,1] neg_lo:[0,1,0] neg_hi:[0,1,0]
	v_pk_add_f32 v[42:43], v[18:19], v[36:37]
	v_pk_add_f32 v[18:19], v[18:19], v[36:37] neg_lo:[0,1] neg_hi:[0,1]
	v_pk_add_f32 v[36:37], v[46:47], v[40:41]
	v_pk_add_f32 v[40:41], v[46:47], v[40:41] neg_lo:[0,1] neg_hi:[0,1]
	s_nop 0
	v_xor_b32_e32 v46, 0x80000000, v41
	v_mov_b32_e32 v47, v40
	v_pk_add_f32 v[40:41], v[42:43], v[36:37]
	v_pk_add_f32 v[36:37], v[42:43], v[36:37] neg_lo:[0,1] neg_hi:[0,1]
	v_pk_add_f32 v[42:43], v[18:19], v[46:47]
	v_pk_add_f32 v[18:19], v[18:19], v[46:47] neg_lo:[0,1] neg_hi:[0,1]
	v_pk_add_f32 v[46:47], v[34:35], v[48:49]
	v_pk_add_f32 v[34:35], v[34:35], v[48:49] neg_lo:[0,1] neg_hi:[0,1]
	v_pk_add_f32 v[48:49], v[28:29], v[38:39]
	v_pk_add_f32 v[28:29], v[28:29], v[38:39] neg_lo:[0,1] neg_hi:[0,1]
	s_nop 0
	v_xor_b32_e32 v38, 0x80000000, v29
	v_mov_b32_e32 v39, v28
	v_pk_add_f32 v[28:29], v[46:47], v[48:49]
	v_pk_add_f32 v[46:47], v[46:47], v[48:49] neg_lo:[0,1] neg_hi:[0,1]
	v_pk_add_f32 v[48:49], v[34:35], v[38:39]
	v_pk_add_f32 v[34:35], v[34:35], v[38:39] neg_lo:[0,1] neg_hi:[0,1]
	v_pk_add_f32 v[38:39], v[20:21], v[44:45]
	v_pk_add_f32 v[20:21], v[20:21], v[44:45] neg_lo:[0,1] neg_hi:[0,1]
	v_pk_add_f32 v[44:45], v[22:23], v[30:31]
	v_pk_add_f32 v[22:23], v[22:23], v[30:31] neg_lo:[0,1] neg_hi:[0,1]
	s_nop 0
	v_pk_mul_f32 v[30:31], v[64:65], v[22:23] op_sel:[0,1] op_sel_hi:[0,0] neg_lo:[0,1]
	v_pk_fma_f32 v[22:23], v[64:65], v[22:23], v[30:31] op_sel_hi:[0,1,1]
	v_pk_add_f32 v[30:31], v[24:25], v[32:33]
	v_pk_add_f32 v[24:25], v[24:25], v[32:33] neg_lo:[0,1] neg_hi:[0,1]
	s_nop 0
	v_xor_b32_e32 v32, 0x80000000, v25
	v_mov_b32_e32 v33, v24
	v_pk_add_f32 v[24:25], v[26:27], v[16:17]
	v_pk_add_f32 v[16:17], v[26:27], v[16:17] neg_lo:[0,1] neg_hi:[0,1]
	s_nop 0
	v_pk_mul_f32 v[26:27], v[64:65], v[16:17] op_sel:[0,1] op_sel_hi:[0,0] neg_lo:[0,1]
	v_pk_fma_f32 v[16:17], v[64:65], v[16:17], v[26:27] op_sel_hi:[0,1,1] neg_lo:[1,0,0] neg_hi:[1,0,0]
	v_pk_add_f32 v[26:27], v[38:39], v[30:31]
	v_pk_add_f32 v[30:31], v[38:39], v[30:31] neg_lo:[0,1] neg_hi:[0,1]
	v_pk_add_f32 v[38:39], v[44:45], v[24:25]
	v_pk_add_f32 v[24:25], v[44:45], v[24:25] neg_lo:[0,1] neg_hi:[0,1]
	s_nop 0
	v_xor_b32_e32 v44, 0x80000000, v25
	v_mov_b32_e32 v45, v24
	v_pk_add_f32 v[24:25], v[26:27], v[38:39]
	v_pk_add_f32 v[26:27], v[26:27], v[38:39] neg_lo:[0,1] neg_hi:[0,1]
	v_pk_add_f32 v[38:39], v[30:31], v[44:45]
	v_pk_add_f32 v[30:31], v[30:31], v[44:45] neg_lo:[0,1] neg_hi:[0,1]
	v_pk_add_f32 v[44:45], v[20:21], v[32:33]
	v_pk_add_f32 v[20:21], v[20:21], v[32:33] neg_lo:[0,1] neg_hi:[0,1]
	v_pk_add_f32 v[32:33], v[22:23], v[16:17]
	v_pk_add_f32 v[16:17], v[22:23], v[16:17] neg_lo:[0,1] neg_hi:[0,1]
	s_nop 0
	v_xor_b32_e32 v22, 0x80000000, v17
	v_mov_b32_e32 v23, v16
	v_pk_add_f32 v[16:17], v[44:45], v[32:33]
	v_pk_add_f32 v[32:33], v[44:45], v[32:33] neg_lo:[0,1] neg_hi:[0,1]
	v_pk_add_f32 v[44:45], v[20:21], v[22:23]
	v_pk_add_f32 v[20:21], v[20:21], v[22:23] neg_lo:[0,1] neg_hi:[0,1]
	ds_write_b64 v10, v[40:41]
	ds_write_b64 v13, v[24:25]
	ds_write_b64 v15, v[28:29]
	ds_write_b64 v50, v[16:17]
	ds_write_b64 v51, v[42:43]
	ds_write_b64 v52, v[38:39]
	ds_write_b64 v53, v[48:49]
	ds_write_b64 v54, v[44:45]
	ds_write_b64 v55, v[36:37]
	ds_write_b64 v56, v[26:27]
	ds_write_b64 v57, v[46:47]
	ds_write_b64 v58, v[32:33]
	ds_write_b64 v59, v[18:19]
	ds_write_b64 v60, v[30:31]
	ds_write_b64 v61, v[34:35]
	ds_write_b64 v62, v[20:21]
	v_mov_b32_e32 v10, v176
	v_mov_b32_e32 v50, v173
	s_waitcnt lgkmcnt(0)
	s_barrier
	v_add_u32_e32 v13, v50, v10
	v_lshl_add_u32 v13, v13, 3, 0
	ds_read2_b64 v[16:19], v13 offset1:16
	v_xad_u32 v15, v50, 1, v10
	v_lshl_add_u32 v15, v15, 3, 0
	s_waitcnt lgkmcnt(0)
	v_pk_fma_f32 v[16:17], v[16:17], 0, v[16:17] op_sel:[1,0,0] op_sel_hi:[0,0,1] neg_hi:[1,0,0]
	v_pk_fma_f32 v[22:23], v[182:183], s[92:93], v[182:183] op_sel:[1,0,0] op_sel_hi:[0,1,1]
	v_pk_mul_f32 v[24:25], v[22:23], v[18:19] op_sel:[1,1] op_sel_hi:[1,0] neg_hi:[0,1]
	s_nop 0
	v_pk_fma_f32 v[18:19], v[18:19], v[22:23], v[24:25] op_sel_hi:[1,0,1]
	v_pk_mul_f32 v[24:25], v[182:183], v[22:23] op_sel:[1,1] op_sel_hi:[0,1] neg_lo:[0,1]
	v_pk_fma_f32 v[26:27], v[182:183], v[22:23], v[24:25] op_sel_hi:[1,0,1]
	ds_read2_b64 v[22:25], v15 offset0:32 offset1:48
	s_waitcnt lgkmcnt(0)
	v_pk_mul_f32 v[28:29], v[22:23], v[26:27] op_sel:[1,1] op_sel_hi:[0,1] neg_hi:[1,0]
	s_nop 0
	v_pk_fma_f32 v[22:23], v[22:23], v[26:27], v[28:29] op_sel_hi:[1,0,1]
	v_pk_mul_f32 v[28:29], v[182:183], v[26:27] op_sel:[1,1] op_sel_hi:[0,1] neg_lo:[0,1]
	v_pk_fma_f32 v[26:27], v[182:183], v[26:27], v[28:29] op_sel_hi:[1,0,1]
	s_nop 0
	v_pk_mul_f32 v[28:29], v[24:25], v[26:27] op_sel:[1,1] op_sel_hi:[0,1] neg_hi:[1,0]
	s_nop 0
	v_pk_fma_f32 v[24:25], v[24:25], v[26:27], v[28:29] op_sel_hi:[1,0,1]
	v_pk_mul_f32 v[28:29], v[182:183], v[26:27] op_sel:[1,1] op_sel_hi:[0,1] neg_lo:[0,1]
	v_pk_fma_f32 v[26:27], v[182:183], v[26:27], v[28:29] op_sel_hi:[1,0,1]
	v_xad_u32 v28, v50, 2, v10
	v_lshl_add_u32 v51, v28, 3, 0
	ds_read2_b64 v[28:31], v51 offset0:64 offset1:80
	v_pk_mul_f32 v[32:33], v[182:183], v[26:27] op_sel:[1,1] op_sel_hi:[0,1] neg_lo:[0,1]
	s_waitcnt lgkmcnt(0)
	v_pk_mul_f32 v[34:35], v[28:29], v[26:27] op_sel:[1,1] op_sel_hi:[0,1] neg_hi:[1,0]
	s_nop 0
	v_pk_fma_f32 v[28:29], v[28:29], v[26:27], v[34:35] op_sel_hi:[1,0,1]
	v_pk_fma_f32 v[34:35], v[182:183], v[26:27], v[32:33] op_sel_hi:[1,0,1]
	s_nop 0
	v_pk_mul_f32 v[26:27], v[30:31], v[34:35] op_sel:[1,1] op_sel_hi:[0,1] neg_hi:[1,0]
	v_pk_fma_f32 v[26:27], v[30:31], v[34:35], v[26:27] op_sel_hi:[1,0,1]
	v_xad_u32 v30, v50, 3, v10
	v_lshl_add_u32 v54, v30, 3, 0
	ds_read2_b64 v[30:33], v54 offset0:96 offset1:112
	v_pk_mul_f32 v[36:37], v[182:183], v[34:35] op_sel:[1,1] op_sel_hi:[0,1] neg_lo:[0,1]
	v_pk_fma_f32 v[34:35], v[182:183], v[34:35], v[36:37] op_sel_hi:[1,0,1]
	s_waitcnt lgkmcnt(0)
	v_pk_mul_f32 v[36:37], v[30:31], v[34:35] op_sel:[1,1] op_sel_hi:[0,1] neg_hi:[1,0]
	s_nop 0
	v_pk_fma_f32 v[30:31], v[30:31], v[34:35], v[36:37] op_sel_hi:[1,0,1]
	v_pk_mul_f32 v[36:37], v[182:183], v[34:35] op_sel:[1,1] op_sel_hi:[0,1] neg_lo:[0,1]
	v_pk_fma_f32 v[34:35], v[182:183], v[34:35], v[36:37] op_sel_hi:[1,0,1]
	s_nop 0
	v_pk_mul_f32 v[36:37], v[32:33], v[34:35] op_sel:[1,1] op_sel_hi:[0,1] neg_hi:[1,0]
	s_nop 0
	v_pk_fma_f32 v[32:33], v[32:33], v[34:35], v[36:37] op_sel_hi:[1,0,1]
	v_pk_mul_f32 v[36:37], v[182:183], v[34:35] op_sel:[1,1] op_sel_hi:[0,1] neg_lo:[0,1]
	v_pk_fma_f32 v[38:39], v[182:183], v[34:35], v[36:37] op_sel_hi:[1,0,1]
	v_xad_u32 v34, v50, 4, v10
	v_lshl_add_u32 v55, v34, 3, 0
	ds_read2_b64 v[34:37], v55 offset0:128 offset1:144
	v_pk_mul_f32 v[40:41], v[182:183], v[38:39] op_sel:[1,1] op_sel_hi:[0,1] neg_lo:[0,1]
	s_waitcnt lgkmcnt(0)
	v_pk_mul_f32 v[42:43], v[34:35], v[38:39] op_sel:[1,1] op_sel_hi:[0,1] neg_hi:[1,0]
	s_nop 0
	v_pk_fma_f32 v[34:35], v[34:35], v[38:39], v[42:43] op_sel_hi:[1,0,1]
	v_pk_fma_f32 v[42:43], v[182:183], v[38:39], v[40:41] op_sel_hi:[1,0,1]
	s_nop 0
	v_pk_mul_f32 v[38:39], v[36:37], v[42:43] op_sel:[1,1] op_sel_hi:[0,1] neg_hi:[1,0]
	v_pk_fma_f32 v[36:37], v[36:37], v[42:43], v[38:39] op_sel_hi:[1,0,1]
	v_xad_u32 v38, v50, 5, v10
	v_lshl_add_u32 v56, v38, 3, 0
	ds_read2_b64 v[38:41], v56 offset0:160 offset1:176
	v_pk_mul_f32 v[44:45], v[182:183], v[42:43] op_sel:[1,1] op_sel_hi:[0,1] neg_lo:[0,1]
	v_pk_fma_f32 v[42:43], v[182:183], v[42:43], v[44:45] op_sel_hi:[1,0,1]
	s_waitcnt lgkmcnt(0)
	v_pk_mul_f32 v[44:45], v[38:39], v[42:43] op_sel:[1,1] op_sel_hi:[0,1] neg_hi:[1,0]
	s_nop 0
	v_pk_fma_f32 v[38:39], v[38:39], v[42:43], v[44:45] op_sel_hi:[1,0,1]
	v_pk_mul_f32 v[44:45], v[182:183], v[42:43] op_sel:[1,1] op_sel_hi:[0,1] neg_lo:[0,1]
	v_pk_fma_f32 v[42:43], v[182:183], v[42:43], v[44:45] op_sel_hi:[1,0,1]
	s_nop 0
	v_pk_mul_f32 v[44:45], v[40:41], v[42:43] op_sel:[1,1] op_sel_hi:[0,1] neg_hi:[1,0]
	s_nop 0
	v_pk_fma_f32 v[40:41], v[40:41], v[42:43], v[44:45] op_sel_hi:[1,0,1]
	v_pk_mul_f32 v[44:45], v[182:183], v[42:43] op_sel:[1,1] op_sel_hi:[0,1] neg_lo:[0,1]
	v_pk_fma_f32 v[42:43], v[182:183], v[42:43], v[44:45] op_sel_hi:[1,0,1]
	v_xad_u32 v44, v50, 6, v10
	v_lshl_add_u32 v57, v44, 3, 0
	ds_read2_b64 v[44:47], v57 offset0:192 offset1:208
	v_pk_mul_f32 v[48:49], v[182:183], v[42:43] op_sel:[1,1] op_sel_hi:[0,1] neg_lo:[0,1]
	s_waitcnt lgkmcnt(0)
	v_pk_mul_f32 v[52:53], v[44:45], v[42:43] op_sel:[1,1] op_sel_hi:[0,1] neg_hi:[1,0]
	s_nop 0
	v_pk_fma_f32 v[44:45], v[44:45], v[42:43], v[52:53] op_sel_hi:[1,0,1]
	v_pk_fma_f32 v[52:53], v[182:183], v[42:43], v[48:49] op_sel_hi:[1,0,1]
	s_nop 0
	v_pk_mul_f32 v[42:43], v[46:47], v[52:53] op_sel:[1,1] op_sel_hi:[0,1] neg_hi:[1,0]
	v_pk_fma_f32 v[42:43], v[46:47], v[52:53], v[42:43] op_sel_hi:[1,0,1]
	v_xad_u32 v46, v50, 7, v10
	v_lshl_add_u32 v58, v46, 3, 0
	ds_read2_b64 v[46:49], v58 offset0:224 offset1:240
	v_pk_mul_f32 v[60:61], v[182:183], v[52:53] op_sel:[1,1] op_sel_hi:[0,1] neg_lo:[0,1]
	v_pk_fma_f32 v[52:53], v[182:183], v[52:53], v[60:61] op_sel_hi:[1,0,1]
	s_waitcnt lgkmcnt(0)
	v_pk_mul_f32 v[60:61], v[46:47], v[52:53] op_sel:[1,1] op_sel_hi:[0,1] neg_hi:[1,0]
	s_nop 0
	v_pk_fma_f32 v[46:47], v[46:47], v[52:53], v[60:61] op_sel_hi:[1,0,1]
	v_pk_mul_f32 v[60:61], v[182:183], v[52:53] op_sel:[1,1] op_sel_hi:[0,1] neg_lo:[0,1]
	v_pk_fma_f32 v[52:53], v[182:183], v[52:53], v[60:61] op_sel_hi:[1,0,1]
	s_nop 0
	v_pk_mul_f32 v[60:61], v[48:49], v[52:53] op_sel:[1,1] op_sel_hi:[0,1] neg_hi:[1,0]
	s_nop 0
	v_pk_fma_f32 v[48:49], v[48:49], v[52:53], v[60:61] op_sel_hi:[1,0,1]
	v_pk_mul_f32 v[60:61], v[182:183], v[52:53] op_sel:[1,1] op_sel_hi:[0,1] neg_lo:[0,1]
	v_pk_fma_f32 v[64:65], v[182:183], v[52:53], v[60:61] op_sel_hi:[1,0,1]
	v_xad_u32 v52, v50, 8, v10
	v_lshl_add_u32 v52, v52, 3, 0
	v_add_u32_e32 v59, 0x800, v52
	ds_read2_b64 v[60:63], v59 offset1:16
	v_pk_mul_f32 v[66:67], v[182:183], v[64:65] op_sel:[1,1] op_sel_hi:[0,1] neg_lo:[0,1]
	v_pk_fma_f32 v[66:67], v[182:183], v[64:65], v[66:67] op_sel_hi:[1,0,1]
	s_waitcnt lgkmcnt(0)
	v_pk_mul_f32 v[52:53], v[60:61], v[64:65] op_sel:[1,1] op_sel_hi:[0,1] neg_hi:[1,0]
	v_pk_fma_f32 v[52:53], v[60:61], v[64:65], v[52:53] op_sel_hi:[1,0,1]
	v_pk_mul_f32 v[60:61], v[62:63], v[66:67] op_sel:[1,1] op_sel_hi:[0,1] neg_hi:[1,0]
	v_pk_fma_f32 v[70:71], v[62:63], v[66:67], v[60:61] op_sel_hi:[1,0,1]
	v_xad_u32 v60, v50, 9, v10
	v_lshl_add_u32 v60, v60, 3, 0
	v_add_u32_e32 v60, 0x800, v60
	ds_read2_b64 v[62:65], v60 offset0:32 offset1:48
	v_pk_mul_f32 v[68:69], v[182:183], v[66:67] op_sel:[1,1] op_sel_hi:[0,1] neg_lo:[0,1]
	v_pk_fma_f32 v[66:67], v[182:183], v[66:67], v[68:69] op_sel_hi:[1,0,1]
	s_waitcnt lgkmcnt(0)
	v_pk_mul_f32 v[68:69], v[62:63], v[66:67] op_sel:[1,1] op_sel_hi:[0,1] neg_hi:[1,0]
	s_nop 0
	v_pk_fma_f32 v[72:73], v[62:63], v[66:67], v[68:69] op_sel_hi:[1,0,1]
	v_pk_mul_f32 v[62:63], v[182:183], v[66:67] op_sel:[1,1] op_sel_hi:[0,1] neg_lo:[0,1]
	v_pk_fma_f32 v[62:63], v[182:183], v[66:67], v[62:63] op_sel_hi:[1,0,1]
	s_nop 0
	v_pk_mul_f32 v[66:67], v[64:65], v[62:63] op_sel:[1,1] op_sel_hi:[0,1] neg_hi:[1,0]
	s_nop 0
	v_pk_fma_f32 v[74:75], v[64:65], v[62:63], v[66:67] op_sel_hi:[1,0,1]
	v_pk_mul_f32 v[64:65], v[182:183], v[62:63] op_sel:[1,1] op_sel_hi:[0,1] neg_lo:[0,1]
	v_pk_fma_f32 v[66:67], v[182:183], v[62:63], v[64:65] op_sel_hi:[1,0,1]
	v_xad_u32 v61, v50, 10, v10
	v_lshl_add_u32 v61, v61, 3, 0
	v_add_u32_e32 v61, 0x800, v61
	ds_read2_b64 v[62:65], v61 offset0:64 offset1:80
	v_pk_mul_f32 v[68:69], v[182:183], v[66:67] op_sel:[1,1] op_sel_hi:[0,1] neg_lo:[0,1]
	v_pk_fma_f32 v[68:69], v[182:183], v[66:67], v[68:69] op_sel_hi:[1,0,1]
	s_waitcnt lgkmcnt(0)
	v_pk_mul_f32 v[76:77], v[62:63], v[66:67] op_sel:[1,1] op_sel_hi:[0,1] neg_hi:[1,0]
	v_pk_fma_f32 v[76:77], v[62:63], v[66:67], v[76:77] op_sel_hi:[1,0,1]
	v_pk_mul_f32 v[62:63], v[64:65], v[68:69] op_sel:[1,1] op_sel_hi:[0,1] neg_hi:[1,0]
	v_pk_fma_f32 v[78:79], v[64:65], v[68:69], v[62:63] op_sel_hi:[1,0,1]
	v_xad_u32 v62, v50, 11, v10
	v_lshl_add_u32 v62, v62, 3, 0
	v_add_u32_e32 v62, 0x800, v62
	ds_read2_b64 v[64:67], v62 offset0:96 offset1:112
	v_pk_mul_f32 v[80:81], v[182:183], v[68:69] op_sel:[1,1] op_sel_hi:[0,1] neg_lo:[0,1]
	v_pk_fma_f32 v[68:69], v[182:183], v[68:69], v[80:81] op_sel_hi:[1,0,1]
	s_waitcnt lgkmcnt(0)
	v_pk_mul_f32 v[80:81], v[64:65], v[68:69] op_sel:[1,1] op_sel_hi:[0,1] neg_hi:[1,0]
	s_nop 0
	v_pk_fma_f32 v[80:81], v[64:65], v[68:69], v[80:81] op_sel_hi:[1,0,1]
	v_pk_mul_f32 v[64:65], v[182:183], v[68:69] op_sel:[1,1] op_sel_hi:[0,1] neg_lo:[0,1]
	v_pk_fma_f32 v[64:65], v[182:183], v[68:69], v[64:65] op_sel_hi:[1,0,1]
	s_nop 0
	v_pk_mul_f32 v[68:69], v[66:67], v[64:65] op_sel:[1,1] op_sel_hi:[0,1] neg_hi:[1,0]
	s_nop 0
	v_pk_fma_f32 v[82:83], v[66:67], v[64:65], v[68:69] op_sel_hi:[1,0,1]
	v_pk_mul_f32 v[66:67], v[182:183], v[64:65] op_sel:[1,1] op_sel_hi:[0,1] neg_lo:[0,1]
	v_pk_fma_f32 v[68:69], v[182:183], v[64:65], v[66:67] op_sel_hi:[1,0,1]
	v_xad_u32 v63, v50, 12, v10
	v_lshl_add_u32 v63, v63, 3, 0
	v_add_u32_e32 v63, 0x800, v63
	ds_read2_b64 v[64:67], v63 offset0:128 offset1:144
	v_pk_mul_f32 v[84:85], v[182:183], v[68:69] op_sel:[1,1] op_sel_hi:[0,1] neg_lo:[0,1]
	v_pk_fma_f32 v[84:85], v[182:183], v[68:69], v[84:85] op_sel_hi:[1,0,1]
	s_waitcnt lgkmcnt(0)
	v_pk_mul_f32 v[86:87], v[64:65], v[68:69] op_sel:[1,1] op_sel_hi:[0,1] neg_hi:[1,0]
	v_pk_fma_f32 v[86:87], v[64:65], v[68:69], v[86:87] op_sel_hi:[1,0,1]
	v_pk_mul_f32 v[64:65], v[66:67], v[84:85] op_sel:[1,1] op_sel_hi:[0,1] neg_hi:[1,0]
	v_pk_fma_f32 v[88:89], v[66:67], v[84:85], v[64:65] op_sel_hi:[1,0,1]
	v_xad_u32 v64, v50, 13, v10
	v_lshl_add_u32 v64, v64, 3, 0
	v_add_u32_e32 v64, 0x800, v64
	ds_read2_b64 v[66:69], v64 offset0:160 offset1:176
	v_pk_mul_f32 v[90:91], v[182:183], v[84:85] op_sel:[1,1] op_sel_hi:[0,1] neg_lo:[0,1]
	v_pk_fma_f32 v[84:85], v[182:183], v[84:85], v[90:91] op_sel_hi:[1,0,1]
	s_waitcnt lgkmcnt(0)
	v_pk_mul_f32 v[90:91], v[66:67], v[84:85] op_sel:[1,1] op_sel_hi:[0,1] neg_hi:[1,0]
	s_nop 0
	v_pk_fma_f32 v[90:91], v[66:67], v[84:85], v[90:91] op_sel_hi:[1,0,1]
	v_pk_mul_f32 v[66:67], v[182:183], v[84:85] op_sel:[1,1] op_sel_hi:[0,1] neg_lo:[0,1]
	v_pk_fma_f32 v[66:67], v[182:183], v[84:85], v[66:67] op_sel_hi:[1,0,1]
	s_nop 0
	v_pk_mul_f32 v[84:85], v[68:69], v[66:67] op_sel:[1,1] op_sel_hi:[0,1] neg_hi:[1,0]
	s_nop 0
	v_pk_fma_f32 v[84:85], v[68:69], v[66:67], v[84:85] op_sel_hi:[1,0,1]
	v_pk_mul_f32 v[68:69], v[182:183], v[66:67] op_sel:[1,1] op_sel_hi:[0,1] neg_lo:[0,1]
	v_pk_fma_f32 v[92:93], v[182:183], v[66:67], v[68:69] op_sel_hi:[1,0,1]
	v_xad_u32 v65, v50, 14, v10
	v_lshl_add_u32 v65, v65, 3, 0
	v_add_u32_e32 v65, 0x800, v65
	ds_read2_b64 v[66:69], v65 offset0:192 offset1:208
	v_pk_mul_f32 v[94:95], v[182:183], v[92:93] op_sel:[1,1] op_sel_hi:[0,1] neg_lo:[0,1]
	v_xad_u32 v10, v50, 15, v10
	s_waitcnt lgkmcnt(0)
	v_pk_mul_f32 v[96:97], v[66:67], v[92:93] op_sel:[1,1] op_sel_hi:[0,1] neg_hi:[1,0]
	v_lshl_add_u32 v10, v10, 3, 0
	v_pk_fma_f32 v[96:97], v[66:67], v[92:93], v[96:97] op_sel_hi:[1,0,1]
	v_pk_fma_f32 v[92:93], v[182:183], v[92:93], v[94:95] op_sel_hi:[1,0,1]
	s_nop 0
	v_pk_mul_f32 v[66:67], v[68:69], v[92:93] op_sel:[1,1] op_sel_hi:[0,1] neg_hi:[1,0]
	v_add_u32_e32 v101, 0x800, v10
	v_pk_fma_f32 v[94:95], v[68:69], v[92:93], v[66:67] op_sel_hi:[1,0,1]
	ds_read2_b64 v[66:69], v101 offset0:224 offset1:240
	v_pk_mul_f32 v[98:99], v[182:183], v[92:93] op_sel:[1,1] op_sel_hi:[0,1] neg_lo:[0,1]
	v_pk_fma_f32 v[92:93], v[182:183], v[92:93], v[98:99] op_sel_hi:[1,0,1]
	s_waitcnt lgkmcnt(0)
	v_pk_mul_f32 v[98:99], v[66:67], v[92:93] op_sel:[1,1] op_sel_hi:[0,1] neg_hi:[1,0]
	s_nop 0
	v_pk_fma_f32 v[66:67], v[66:67], v[92:93], v[98:99] op_sel_hi:[1,0,1]
	v_pk_mul_f32 v[98:99], v[182:183], v[92:93] op_sel:[1,1] op_sel_hi:[0,1] neg_lo:[0,1]
	v_pk_fma_f32 v[20:21], v[182:183], v[92:93], v[98:99] op_sel_hi:[1,0,1]
	s_nop 0
	v_pk_mul_f32 v[92:93], v[68:69], v[20:21] op_sel:[1,1] op_sel_hi:[0,1] neg_hi:[1,0]
	s_nop 0
	v_pk_fma_f32 v[68:69], v[68:69], v[20:21], v[92:93] op_sel_hi:[1,0,1]
	v_pk_add_f32 v[104:105], v[16:17], v[52:53]
	v_pk_add_f32 v[16:17], v[16:17], v[52:53] neg_lo:[0,1] neg_hi:[0,1]
	v_pk_add_f32 v[52:53], v[18:19], v[70:71]
	v_pk_add_f32 v[18:19], v[18:19], v[70:71] neg_lo:[0,1] neg_hi:[0,1]
	v_mov_b32_e32 v92, v165
	v_mov_b32_e32 v20, v166
	v_mov_b32_e32 v98, v167
	v_mov_b32_e32 v10, v168
	v_mov_b32_e32 v100, v169
	v_mov_b32_e32 v50, v170
	v_mov_b32_e32 v102, v171
	v_mov_b32_e32 v21, v172
	v_pk_mul_f32 v[70:71], v[102:103], v[18:19] op_sel:[0,1] op_sel_hi:[0,0] neg_lo:[0,1]
	v_pk_fma_f32 v[18:19], v[92:93], v[18:19], v[70:71] op_sel_hi:[0,1,1]
	v_pk_add_f32 v[70:71], v[22:23], v[72:73]
	v_pk_add_f32 v[22:23], v[22:23], v[72:73] neg_lo:[0,1] neg_hi:[0,1]
	s_nop 0
	v_pk_mul_f32 v[72:73], v[50:51], v[22:23] op_sel:[0,1] op_sel_hi:[0,0] neg_lo:[0,1]
	v_pk_fma_f32 v[22:23], v[20:21], v[22:23], v[72:73] op_sel_hi:[0,1,1]
	v_pk_add_f32 v[72:73], v[24:25], v[74:75]
	v_pk_add_f32 v[24:25], v[24:25], v[74:75] neg_lo:[0,1] neg_hi:[0,1]
	s_nop 0
	v_pk_mul_f32 v[74:75], v[100:101], v[24:25] op_sel:[0,1] op_sel_hi:[0,0] neg_lo:[0,1]
	v_pk_fma_f32 v[24:25], v[98:99], v[24:25], v[74:75] op_sel_hi:[0,1,1]
	v_pk_add_f32 v[74:75], v[28:29], v[76:77]
	v_pk_add_f32 v[28:29], v[28:29], v[76:77] neg_lo:[0,1] neg_hi:[0,1]
	s_nop 0
	v_pk_mul_f32 v[76:77], v[10:11], v[28:29] op_sel:[0,1] op_sel_hi:[0,0] neg_lo:[0,1]
	v_pk_fma_f32 v[28:29], v[10:11], v[28:29], v[76:77] op_sel_hi:[0,1,1]
	v_pk_add_f32 v[76:77], v[26:27], v[78:79]
	v_pk_add_f32 v[26:27], v[26:27], v[78:79] neg_lo:[0,1] neg_hi:[0,1]
	s_nop 0
	v_pk_mul_f32 v[78:79], v[98:99], v[26:27] op_sel:[0,1] op_sel_hi:[0,0] neg_lo:[0,1]
	v_pk_fma_f32 v[26:27], v[100:101], v[26:27], v[78:79] op_sel_hi:[0,1,1]
	v_pk_add_f32 v[78:79], v[30:31], v[80:81]
	v_pk_add_f32 v[30:31], v[30:31], v[80:81] neg_lo:[0,1] neg_hi:[0,1]
	s_nop 0
	v_pk_mul_f32 v[80:81], v[20:21], v[30:31] op_sel:[0,1] op_sel_hi:[0,0] neg_lo:[0,1]
	v_pk_fma_f32 v[30:31], v[50:51], v[30:31], v[80:81] op_sel_hi:[0,1,1]
	v_pk_add_f32 v[80:81], v[32:33], v[82:83]
	v_pk_add_f32 v[32:33], v[32:33], v[82:83] neg_lo:[0,1] neg_hi:[0,1]
	s_nop 0
	v_pk_mul_f32 v[82:83], v[92:93], v[32:33] op_sel:[0,1] op_sel_hi:[0,0] neg_lo:[0,1]
	v_pk_fma_f32 v[32:33], v[102:103], v[32:33], v[82:83] op_sel_hi:[0,1,1]
	v_pk_add_f32 v[82:83], v[34:35], v[86:87]
	v_pk_add_f32 v[34:35], v[34:35], v[86:87] neg_lo:[0,1] neg_hi:[0,1]
	s_nop 0
	v_xor_b32_e32 v86, 0x80000000, v35
	v_mov_b32_e32 v87, v34
	v_pk_add_f32 v[34:35], v[36:37], v[88:89]
	v_pk_add_f32 v[36:37], v[36:37], v[88:89] neg_lo:[0,1] neg_hi:[0,1]
	s_nop 0
	v_pk_mul_f32 v[88:89], v[92:93], v[36:37] op_sel:[0,1] op_sel_hi:[0,0] neg_lo:[0,1]
	v_pk_fma_f32 v[36:37], v[102:103], v[36:37], v[88:89] op_sel_hi:[0,1,1] neg_lo:[1,0,0] neg_hi:[1,0,0]
	v_pk_add_f32 v[88:89], v[38:39], v[90:91]
	v_pk_add_f32 v[38:39], v[38:39], v[90:91] neg_lo:[0,1] neg_hi:[0,1]
	s_nop 0
	v_pk_mul_f32 v[90:91], v[20:21], v[38:39] op_sel:[0,1] op_sel_hi:[0,0] neg_lo:[0,1]
	v_pk_fma_f32 v[38:39], v[50:51], v[38:39], v[90:91] op_sel_hi:[0,1,1] neg_lo:[1,0,0] neg_hi:[1,0,0]
	v_pk_add_f32 v[90:91], v[40:41], v[84:85]
	v_pk_add_f32 v[40:41], v[40:41], v[84:85] neg_lo:[0,1] neg_hi:[0,1]
	s_nop 0
	v_pk_mul_f32 v[84:85], v[98:99], v[40:41] op_sel:[0,1] op_sel_hi:[0,0] neg_lo:[0,1]
	v_pk_fma_f32 v[40:41], v[100:101], v[40:41], v[84:85] op_sel_hi:[0,1,1] neg_lo:[1,0,0] neg_hi:[1,0,0]
	v_pk_add_f32 v[84:85], v[44:45], v[96:97]
	v_pk_add_f32 v[44:45], v[44:45], v[96:97] neg_lo:[0,1] neg_hi:[0,1]
	s_nop 0
	v_pk_mul_f32 v[96:97], v[10:11], v[44:45] op_sel:[0,1] op_sel_hi:[0,0] neg_lo:[0,1]
	v_pk_fma_f32 v[44:45], v[10:11], v[44:45], v[96:97] op_sel_hi:[0,1,1] neg_lo:[1,0,0] neg_hi:[1,0,0]
	v_pk_add_f32 v[96:97], v[42:43], v[94:95]
	v_pk_add_f32 v[42:43], v[42:43], v[94:95] neg_lo:[0,1] neg_hi:[0,1]
	s_nop 0
	v_pk_mul_f32 v[94:95], v[100:101], v[42:43] op_sel:[0,1] op_sel_hi:[0,0] neg_lo:[0,1]
	v_pk_fma_f32 v[42:43], v[98:99], v[42:43], v[94:95] op_sel_hi:[0,1,1] neg_lo:[1,0,0] neg_hi:[1,0,0]
	v_pk_add_f32 v[94:95], v[46:47], v[66:67]
	v_pk_add_f32 v[46:47], v[46:47], v[66:67] neg_lo:[0,1] neg_hi:[0,1]
	s_nop 0
	v_pk_mul_f32 v[66:67], v[50:51], v[46:47] op_sel:[0,1] op_sel_hi:[0,0] neg_lo:[0,1]
	v_pk_fma_f32 v[46:47], v[20:21], v[46:47], v[66:67] op_sel_hi:[0,1,1] neg_lo:[1,0,0] neg_hi:[1,0,0]
	v_pk_add_f32 v[66:67], v[48:49], v[68:69]
	v_pk_add_f32 v[48:49], v[48:49], v[68:69] neg_lo:[0,1] neg_hi:[0,1]
	s_nop 0
	v_pk_mul_f32 v[68:69], v[102:103], v[48:49] op_sel:[0,1] op_sel_hi:[0,0] neg_lo:[0,1]
	v_pk_fma_f32 v[48:49], v[92:93], v[48:49], v[68:69] op_sel_hi:[0,1,1] neg_lo:[1,0,0] neg_hi:[1,0,0]
	v_pk_add_f32 v[92:93], v[52:53], v[34:35]
	v_pk_add_f32 v[34:35], v[52:53], v[34:35] neg_lo:[0,1] neg_hi:[0,1]
	v_pk_add_f32 v[68:69], v[104:105], v[82:83]
	v_pk_mul_f32 v[52:53], v[50:51], v[34:35] op_sel:[0,1] op_sel_hi:[0,0] neg_lo:[0,1]
	v_pk_fma_f32 v[34:35], v[20:21], v[34:35], v[52:53] op_sel_hi:[0,1,1]
	v_pk_add_f32 v[52:53], v[70:71], v[88:89]
	v_pk_add_f32 v[70:71], v[70:71], v[88:89] neg_lo:[0,1] neg_hi:[0,1]
	v_pk_add_f32 v[82:83], v[104:105], v[82:83] neg_lo:[0,1] neg_hi:[0,1]
	v_pk_mul_f32 v[88:89], v[10:11], v[70:71] op_sel:[0,1] op_sel_hi:[0,0] neg_lo:[0,1]
	v_pk_fma_f32 v[70:71], v[10:11], v[70:71], v[88:89] op_sel_hi:[0,1,1]
	v_pk_add_f32 v[88:89], v[72:73], v[90:91]
	v_pk_add_f32 v[72:73], v[72:73], v[90:91] neg_lo:[0,1] neg_hi:[0,1]
	s_nop 0
	v_pk_mul_f32 v[90:91], v[20:21], v[72:73] op_sel:[0,1] op_sel_hi:[0,0] neg_lo:[0,1]
	v_pk_fma_f32 v[72:73], v[50:51], v[72:73], v[90:91] op_sel_hi:[0,1,1]
	v_pk_add_f32 v[90:91], v[74:75], v[84:85]
	v_pk_add_f32 v[74:75], v[74:75], v[84:85] neg_lo:[0,1] neg_hi:[0,1]
	s_nop 0
	v_xor_b32_e32 v84, 0x80000000, v75
	v_mov_b32_e32 v85, v74
	v_pk_add_f32 v[74:75], v[76:77], v[96:97]
	v_pk_add_f32 v[76:77], v[76:77], v[96:97] neg_lo:[0,1] neg_hi:[0,1]
	s_nop 0
	v_pk_mul_f32 v[96:97], v[20:21], v[76:77] op_sel:[0,1] op_sel_hi:[0,0] neg_lo:[0,1]
	v_pk_fma_f32 v[76:77], v[50:51], v[76:77], v[96:97] op_sel_hi:[0,1,1] neg_lo:[1,0,0] neg_hi:[1,0,0]
	v_pk_add_f32 v[96:97], v[78:79], v[94:95]
	v_pk_add_f32 v[78:79], v[78:79], v[94:95] neg_lo:[0,1] neg_hi:[0,1]
	s_nop 0
	v_pk_mul_f32 v[94:95], v[10:11], v[78:79] op_sel:[0,1] op_sel_hi:[0,0] neg_lo:[0,1]
	v_pk_fma_f32 v[78:79], v[10:11], v[78:79], v[94:95] op_sel_hi:[0,1,1] neg_lo:[1,0,0] neg_hi:[1,0,0]
	v_pk_add_f32 v[94:95], v[80:81], v[66:67]
	v_pk_add_f32 v[66:67], v[80:81], v[66:67] neg_lo:[0,1] neg_hi:[0,1]
	s_nop 0
	v_pk_mul_f32 v[80:81], v[50:51], v[66:67] op_sel:[0,1] op_sel_hi:[0,0] neg_lo:[0,1]
	v_pk_fma_f32 v[66:67], v[20:21], v[66:67], v[80:81] op_sel_hi:[0,1,1] neg_lo:[1,0,0] neg_hi:[1,0,0]
	v_pk_add_f32 v[80:81], v[68:69], v[90:91]
	v_pk_add_f32 v[68:69], v[68:69], v[90:91] neg_lo:[0,1] neg_hi:[0,1]
	v_pk_add_f32 v[90:91], v[92:93], v[74:75]
	v_pk_add_f32 v[74:75], v[92:93], v[74:75] neg_lo:[0,1] neg_hi:[0,1]
	s_nop 0
	v_pk_mul_f32 v[92:93], v[10:11], v[74:75] op_sel:[0,1] op_sel_hi:[0,0] neg_lo:[0,1]
	v_pk_fma_f32 v[74:75], v[10:11], v[74:75], v[92:93] op_sel_hi:[0,1,1]
	v_pk_add_f32 v[92:93], v[52:53], v[96:97]
	v_pk_add_f32 v[52:53], v[52:53], v[96:97] neg_lo:[0,1] neg_hi:[0,1]
	s_nop 0
	v_xor_b32_e32 v96, 0x80000000, v53
	v_mov_b32_e32 v97, v52
	v_pk_add_f32 v[52:53], v[88:89], v[94:95]
	v_pk_add_f32 v[88:89], v[88:89], v[94:95] neg_lo:[0,1] neg_hi:[0,1]
	s_nop 0
	v_pk_mul_f32 v[94:95], v[10:11], v[88:89] op_sel:[0,1] op_sel_hi:[0,0] neg_lo:[0,1]
	v_pk_fma_f32 v[88:89], v[10:11], v[88:89], v[94:95] op_sel_hi:[0,1,1] neg_lo:[1,0,0] neg_hi:[1,0,0]
	v_pk_add_f32 v[94:95], v[80:81], v[92:93]
	v_pk_add_f32 v[80:81], v[80:81], v[92:93] neg_lo:[0,1] neg_hi:[0,1]
	v_pk_add_f32 v[92:93], v[90:91], v[52:53]
	v_pk_add_f32 v[52:53], v[90:91], v[52:53] neg_lo:[0,1] neg_hi:[0,1]
	s_nop 0
	v_xor_b32_e32 v90, 0x80000000, v53
	v_mov_b32_e32 v91, v52
	v_pk_add_f32 v[52:53], v[94:95], v[92:93]
	v_pk_add_f32 v[92:93], v[94:95], v[92:93] neg_lo:[0,1] neg_hi:[0,1]
	v_pk_add_f32 v[94:95], v[80:81], v[90:91]
	v_pk_add_f32 v[80:81], v[80:81], v[90:91] neg_lo:[0,1] neg_hi:[0,1]
	v_pk_add_f32 v[90:91], v[68:69], v[96:97]
	v_pk_add_f32 v[68:69], v[68:69], v[96:97] neg_lo:[0,1] neg_hi:[0,1]
	v_pk_add_f32 v[96:97], v[74:75], v[88:89]
	v_pk_add_f32 v[74:75], v[74:75], v[88:89] neg_lo:[0,1] neg_hi:[0,1]
	s_nop 0
	v_xor_b32_e32 v88, 0x80000000, v75
	v_mov_b32_e32 v89, v74
	v_pk_add_f32 v[74:75], v[90:91], v[96:97]
	v_pk_add_f32 v[90:91], v[90:91], v[96:97] neg_lo:[0,1] neg_hi:[0,1]
	v_pk_add_f32 v[96:97], v[68:69], v[88:89]
	v_pk_add_f32 v[68:69], v[68:69], v[88:89] neg_lo:[0,1] neg_hi:[0,1]
	v_pk_add_f32 v[88:89], v[82:83], v[84:85]
	v_pk_add_f32 v[82:83], v[82:83], v[84:85] neg_lo:[0,1] neg_hi:[0,1]
	v_pk_add_f32 v[84:85], v[34:35], v[76:77]
	v_pk_add_f32 v[34:35], v[34:35], v[76:77] neg_lo:[0,1] neg_hi:[0,1]
	s_nop 0
	v_pk_mul_f32 v[76:77], v[10:11], v[34:35] op_sel:[0,1] op_sel_hi:[0,0] neg_lo:[0,1]
	v_pk_fma_f32 v[34:35], v[10:11], v[34:35], v[76:77] op_sel_hi:[0,1,1]
	v_pk_add_f32 v[76:77], v[70:71], v[78:79]
	v_pk_add_f32 v[70:71], v[70:71], v[78:79] neg_lo:[0,1] neg_hi:[0,1]
	s_nop 0
	v_xor_b32_e32 v78, 0x80000000, v71
	v_mov_b32_e32 v79, v70
	v_pk_add_f32 v[70:71], v[72:73], v[66:67]
	v_pk_add_f32 v[66:67], v[72:73], v[66:67] neg_lo:[0,1] neg_hi:[0,1]
	s_nop 0
	v_pk_mul_f32 v[72:73], v[10:11], v[66:67] op_sel:[0,1] op_sel_hi:[0,0] neg_lo:[0,1]
	v_pk_fma_f32 v[66:67], v[10:11], v[66:67], v[72:73] op_sel_hi:[0,1,1] neg_lo:[1,0,0] neg_hi:[1,0,0]
	v_pk_add_f32 v[72:73], v[88:89], v[76:77]
	v_pk_add_f32 v[76:77], v[88:89], v[76:77] neg_lo:[0,1] neg_hi:[0,1]
	v_pk_add_f32 v[88:89], v[84:85], v[70:71]
	v_pk_add_f32 v[70:71], v[84:85], v[70:71] neg_lo:[0,1] neg_hi:[0,1]
	s_nop 0
	v_xor_b32_e32 v84, 0x80000000, v71
	v_mov_b32_e32 v85, v70
	v_pk_add_f32 v[70:71], v[72:73], v[88:89]
	v_pk_add_f32 v[72:73], v[72:73], v[88:89] neg_lo:[0,1] neg_hi:[0,1]
	v_pk_add_f32 v[88:89], v[76:77], v[84:85]
	v_pk_add_f32 v[76:77], v[76:77], v[84:85] neg_lo:[0,1] neg_hi:[0,1]
	v_pk_add_f32 v[84:85], v[82:83], v[78:79]
	v_pk_add_f32 v[78:79], v[82:83], v[78:79] neg_lo:[0,1] neg_hi:[0,1]
	v_pk_add_f32 v[82:83], v[34:35], v[66:67]
	v_pk_add_f32 v[34:35], v[34:35], v[66:67] neg_lo:[0,1] neg_hi:[0,1]
	s_nop 0
	v_xor_b32_e32 v66, 0x80000000, v35
	v_mov_b32_e32 v67, v34
	v_pk_add_f32 v[34:35], v[84:85], v[82:83]
	v_pk_add_f32 v[82:83], v[84:85], v[82:83] neg_lo:[0,1] neg_hi:[0,1]
	v_pk_add_f32 v[84:85], v[78:79], v[66:67]
	v_pk_add_f32 v[66:67], v[78:79], v[66:67] neg_lo:[0,1] neg_hi:[0,1]
	v_pk_add_f32 v[78:79], v[16:17], v[86:87]
	v_pk_add_f32 v[16:17], v[16:17], v[86:87] neg_lo:[0,1] neg_hi:[0,1]
	v_pk_add_f32 v[86:87], v[18:19], v[36:37]
	v_pk_add_f32 v[18:19], v[18:19], v[36:37] neg_lo:[0,1] neg_hi:[0,1]
	s_nop 0
	v_pk_mul_f32 v[36:37], v[50:51], v[18:19] op_sel:[0,1] op_sel_hi:[0,0] neg_lo:[0,1]
	v_pk_fma_f32 v[18:19], v[20:21], v[18:19], v[36:37] op_sel_hi:[0,1,1]
	v_pk_add_f32 v[36:37], v[22:23], v[38:39]
	v_pk_add_f32 v[22:23], v[22:23], v[38:39] neg_lo:[0,1] neg_hi:[0,1]
	s_nop 0
	v_pk_mul_f32 v[38:39], v[10:11], v[22:23] op_sel:[0,1] op_sel_hi:[0,0] neg_lo:[0,1]
	v_pk_fma_f32 v[22:23], v[10:11], v[22:23], v[38:39] op_sel_hi:[0,1,1]
	v_pk_add_f32 v[38:39], v[24:25], v[40:41]
	v_pk_add_f32 v[24:25], v[24:25], v[40:41] neg_lo:[0,1] neg_hi:[0,1]
	s_nop 0
	v_pk_mul_f32 v[40:41], v[20:21], v[24:25] op_sel:[0,1] op_sel_hi:[0,0] neg_lo:[0,1]
	v_pk_fma_f32 v[24:25], v[50:51], v[24:25], v[40:41] op_sel_hi:[0,1,1]
	v_pk_add_f32 v[40:41], v[28:29], v[44:45]
	v_pk_add_f32 v[28:29], v[28:29], v[44:45] neg_lo:[0,1] neg_hi:[0,1]
	s_nop 0
	v_xor_b32_e32 v44, 0x80000000, v29
	v_mov_b32_e32 v45, v28
	v_pk_add_f32 v[28:29], v[26:27], v[42:43]
	v_pk_add_f32 v[26:27], v[26:27], v[42:43] neg_lo:[0,1] neg_hi:[0,1]
	s_nop 0
	v_pk_mul_f32 v[42:43], v[20:21], v[26:27] op_sel:[0,1] op_sel_hi:[0,0] neg_lo:[0,1]
	v_pk_fma_f32 v[26:27], v[50:51], v[26:27], v[42:43] op_sel_hi:[0,1,1] neg_lo:[1,0,0] neg_hi:[1,0,0]
	v_pk_add_f32 v[42:43], v[30:31], v[46:47]
	v_pk_add_f32 v[30:31], v[30:31], v[46:47] neg_lo:[0,1] neg_hi:[0,1]
	s_nop 0
	v_pk_mul_f32 v[46:47], v[10:11], v[30:31] op_sel:[0,1] op_sel_hi:[0,0] neg_lo:[0,1]
	v_pk_fma_f32 v[30:31], v[10:11], v[30:31], v[46:47] op_sel_hi:[0,1,1] neg_lo:[1,0,0] neg_hi:[1,0,0]
	v_pk_add_f32 v[46:47], v[32:33], v[48:49]
	v_pk_add_f32 v[32:33], v[32:33], v[48:49] neg_lo:[0,1] neg_hi:[0,1]
	s_nop 0
	v_pk_mul_f32 v[48:49], v[50:51], v[32:33] op_sel:[0,1] op_sel_hi:[0,0] neg_lo:[0,1]
	v_pk_fma_f32 v[20:21], v[20:21], v[32:33], v[48:49] op_sel_hi:[0,1,1] neg_lo:[1,0,0] neg_hi:[1,0,0]
	v_pk_add_f32 v[48:49], v[86:87], v[28:29]
	v_pk_add_f32 v[28:29], v[86:87], v[28:29] neg_lo:[0,1] neg_hi:[0,1]
	v_pk_add_f32 v[32:33], v[78:79], v[40:41]
	v_pk_add_f32 v[40:41], v[78:79], v[40:41] neg_lo:[0,1] neg_hi:[0,1]
	v_pk_mul_f32 v[78:79], v[10:11], v[28:29] op_sel:[0,1] op_sel_hi:[0,0] neg_lo:[0,1]
	v_pk_fma_f32 v[28:29], v[10:11], v[28:29], v[78:79] op_sel_hi:[0,1,1]
	v_pk_add_f32 v[78:79], v[36:37], v[42:43]
	v_pk_add_f32 v[36:37], v[36:37], v[42:43] neg_lo:[0,1] neg_hi:[0,1]
	s_nop 0
	v_xor_b32_e32 v42, 0x80000000, v37
	v_mov_b32_e32 v43, v36
	v_pk_add_f32 v[36:37], v[38:39], v[46:47]
	v_pk_add_f32 v[38:39], v[38:39], v[46:47] neg_lo:[0,1] neg_hi:[0,1]
	s_nop 0
	v_pk_mul_f32 v[46:47], v[10:11], v[38:39] op_sel:[0,1] op_sel_hi:[0,0] neg_lo:[0,1]
	v_pk_fma_f32 v[38:39], v[10:11], v[38:39], v[46:47] op_sel_hi:[0,1,1] neg_lo:[1,0,0] neg_hi:[1,0,0]
	v_pk_add_f32 v[46:47], v[32:33], v[78:79]
	v_pk_add_f32 v[32:33], v[32:33], v[78:79] neg_lo:[0,1] neg_hi:[0,1]
	v_pk_add_f32 v[78:79], v[48:49], v[36:37]
	v_pk_add_f32 v[36:37], v[48:49], v[36:37] neg_lo:[0,1] neg_hi:[0,1]
	s_nop 0
	v_pk_add_f32 v[86:87], v[32:33], v[36:37] op_sel:[0,1] op_sel_hi:[1,0] neg_lo:[0,1]
	v_pk_add_f32 v[32:33], v[32:33], v[36:37] op_sel:[0,1] op_sel_hi:[1,0] neg_hi:[0,1]
	v_pk_add_f32 v[48:49], v[40:41], v[42:43]
	v_pk_add_f32 v[40:41], v[40:41], v[42:43] neg_lo:[0,1] neg_hi:[0,1]
	v_pk_add_f32 v[42:43], v[28:29], v[38:39]
	v_pk_add_f32 v[28:29], v[28:29], v[38:39] neg_lo:[0,1] neg_hi:[0,1]
	v_pk_add_f32 v[36:37], v[46:47], v[78:79] neg_lo:[0,1] neg_hi:[0,1]
	v_xor_b32_e32 v38, 0x80000000, v29
	v_mov_b32_e32 v39, v28
	v_pk_add_f32 v[28:29], v[48:49], v[42:43]
	v_pk_add_f32 v[42:43], v[48:49], v[42:43] neg_lo:[0,1] neg_hi:[0,1]
	v_pk_add_f32 v[48:49], v[40:41], v[38:39]
	v_pk_add_f32 v[38:39], v[40:41], v[38:39] neg_lo:[0,1] neg_hi:[0,1]
	v_pk_add_f32 v[40:41], v[16:17], v[44:45]
	v_pk_add_f32 v[16:17], v[16:17], v[44:45] neg_lo:[0,1] neg_hi:[0,1]
	v_pk_add_f32 v[44:45], v[18:19], v[26:27]
	v_pk_add_f32 v[18:19], v[18:19], v[26:27] neg_lo:[0,1] neg_hi:[0,1]
	s_nop 0
	v_pk_mul_f32 v[26:27], v[10:11], v[18:19] op_sel:[0,1] op_sel_hi:[0,0] neg_lo:[0,1]
	v_pk_fma_f32 v[18:19], v[10:11], v[18:19], v[26:27] op_sel_hi:[0,1,1]
	v_pk_add_f32 v[26:27], v[22:23], v[30:31]
	v_pk_add_f32 v[22:23], v[22:23], v[30:31] neg_lo:[0,1] neg_hi:[0,1]
	s_nop 0
	v_xor_b32_e32 v30, 0x80000000, v23
	v_mov_b32_e32 v31, v22
	v_pk_add_f32 v[22:23], v[24:25], v[20:21]
	v_pk_add_f32 v[20:21], v[24:25], v[20:21] neg_lo:[0,1] neg_hi:[0,1]
	s_nop 0
	v_pk_mul_f32 v[24:25], v[10:11], v[20:21] op_sel:[0,1] op_sel_hi:[0,0] neg_lo:[0,1]
	v_pk_fma_f32 v[20:21], v[10:11], v[20:21], v[24:25] op_sel_hi:[0,1,1] neg_lo:[1,0,0] neg_hi:[1,0,0]
	v_pk_add_f32 v[24:25], v[40:41], v[26:27]
	v_pk_add_f32 v[26:27], v[40:41], v[26:27] neg_lo:[0,1] neg_hi:[0,1]
	v_pk_add_f32 v[40:41], v[44:45], v[22:23]
	v_pk_add_f32 v[22:23], v[44:45], v[22:23] neg_lo:[0,1] neg_hi:[0,1]
	s_nop 0
	v_xor_b32_e32 v44, 0x80000000, v23
	v_mov_b32_e32 v45, v22
	v_pk_add_f32 v[22:23], v[24:25], v[40:41]
	v_pk_add_f32 v[24:25], v[24:25], v[40:41] neg_lo:[0,1] neg_hi:[0,1]
	v_pk_add_f32 v[40:41], v[26:27], v[44:45]
	v_pk_add_f32 v[26:27], v[26:27], v[44:45] neg_lo:[0,1] neg_hi:[0,1]
	v_pk_add_f32 v[44:45], v[16:17], v[30:31]
	v_pk_add_f32 v[16:17], v[16:17], v[30:31] neg_lo:[0,1] neg_hi:[0,1]
	v_pk_add_f32 v[30:31], v[18:19], v[20:21]
	v_pk_add_f32 v[18:19], v[18:19], v[20:21] neg_lo:[0,1] neg_hi:[0,1]
	s_nop 0
	v_xor_b32_e32 v20, 0x80000000, v19
	v_mov_b32_e32 v21, v18
	v_pk_add_f32 v[18:19], v[44:45], v[30:31]
	v_pk_add_f32 v[30:31], v[44:45], v[30:31] neg_lo:[0,1] neg_hi:[0,1]
	v_pk_add_f32 v[44:45], v[16:17], v[20:21]
	v_pk_add_f32 v[16:17], v[16:17], v[20:21] neg_lo:[0,1] neg_hi:[0,1]
	v_pk_add_f32 v[20:21], v[46:47], v[78:79]
	ds_write2_b64 v13, v[52:53], v[20:21] offset1:16
	ds_write2_b64 v15, v[70:71], v[22:23] offset0:32 offset1:48
	ds_write2_b64 v51, v[74:75], v[28:29] offset0:64 offset1:80
	ds_write2_b64 v54, v[34:35], v[18:19] offset0:96 offset1:112
	ds_write2_b64 v55, v[94:95], v[86:87] offset0:128 offset1:144
	ds_write2_b64 v56, v[88:89], v[40:41] offset0:160 offset1:176
	ds_write2_b64 v57, v[96:97], v[48:49] offset0:192 offset1:208
	ds_write2_b64 v58, v[84:85], v[44:45] offset0:224 offset1:240
	ds_write2_b64 v59, v[92:93], v[36:37] offset1:16
	ds_write2_b64 v60, v[72:73], v[24:25] offset0:32 offset1:48
	ds_write2_b64 v61, v[90:91], v[42:43] offset0:64 offset1:80
	ds_write2_b64 v62, v[82:83], v[30:31] offset0:96 offset1:112
	ds_write2_b64 v63, v[80:81], v[32:33] offset0:128 offset1:144
	ds_write2_b64 v64, v[76:77], v[26:27] offset0:160 offset1:176
	ds_write2_b64 v65, v[68:69], v[38:39] offset0:192 offset1:208
	ds_write2_b64 v101, v[66:67], v[16:17] offset0:224 offset1:240
	v_mov_b32_e32 v10, v174
	s_waitcnt lgkmcnt(0)
	s_barrier
	v_lshl_add_u32 v10, v10, 3, 0
	ds_read_b64 v[16:17], v10
	ds_read_b64 v[80:81], v10 offset:4224
	ds_read_b64 v[78:79], v10 offset:8448
	ds_read_b64 v[76:77], v10 offset:12672
	ds_read_b64 v[74:75], v10 offset:16896
	ds_read_b64 v[72:73], v10 offset:21120
	ds_read_b64 v[70:71], v10 offset:25344
	ds_read_b64 v[68:69], v10 offset:29568
	ds_read_b64 v[24:25], v10 offset:33792
	ds_read_b64 v[62:63], v10 offset:38016
	ds_read_b64 v[60:61], v10 offset:42240
	ds_read_b64 v[58:59], v10 offset:46464
	ds_read_b64 v[54:55], v10 offset:50688
	ds_read_b64 v[50:51], v10 offset:54912
	ds_read_b64 v[46:47], v10 offset:59136
	ds_read_b64 v[44:45], v10 offset:63360
	v_add_u32_e32 v13, 0x10800, v10
	v_add_u32_e32 v15, 0x11880, v10
	v_add_u32_e32 v20, 0x12900, v10
	v_add_u32_e32 v21, 0x13980, v10
	ds_read_b64 v[18:19], v13
	ds_read_b64 v[66:67], v15
	ds_read_b64 v[64:65], v20
	ds_read_b64 v[38:39], v21
	v_add_u32_e32 v13, 0x14a00, v10
	v_add_u32_e32 v15, 0x15a80, v10
	v_add_u32_e32 v20, 0x16b00, v10
	v_add_u32_e32 v21, 0x17b80, v10
	ds_read_b64 v[30:31], v13
	ds_read_b64 v[56:57], v15
	ds_read_b64 v[52:53], v20
	ds_read_b64 v[48:49], v21
	v_add_u32_e32 v13, 0x18c00, v10
	v_add_u32_e32 v15, 0x19c80, v10
	v_add_u32_e32 v20, 0x1ad00, v10
	v_add_u32_e32 v21, 0x1bd80, v10
	ds_read_b64 v[82:83], v13
	ds_read_b64 v[42:43], v15
	ds_read_b64 v[40:41], v20
	ds_read_b64 v[36:37], v21
	v_add_u32_e32 v13, 0x1ce00, v10
	v_add_u32_e32 v15, 0x1de80, v10
	v_add_u32_e32 v20, 0x1ef00, v10
	v_add_u32_e32 v10, 0x1ff80, v10
	ds_read_b64 v[34:35], v13
	ds_read_b64 v[32:33], v15
	ds_read_b64 v[28:29], v20
	ds_read_b64 v[26:27], v10
	v_pk_fma_f32 v[84:85], v[180:181], s[92:93], v[180:181] op_sel:[1,0,0] op_sel_hi:[0,1,1]
	v_pk_mul_f32 v[20:21], v[180:181], v[84:85] op_sel:[1,1] op_sel_hi:[0,1] neg_lo:[0,1]
	v_pk_fma_f32 v[86:87], v[180:181], v[84:85], v[20:21] op_sel_hi:[1,0,1]
	v_pk_mul_f32 v[20:21], v[180:181], v[86:87] op_sel:[1,1] op_sel_hi:[0,1] neg_lo:[0,1]
	v_pk_fma_f32 v[88:89], v[180:181], v[86:87], v[20:21] op_sel_hi:[1,0,1]
	s_waitcnt lgkmcnt(14)
	v_fmac_f32_e32 v16, 0, v17
	v_pk_mul_f32 v[20:21], v[180:181], v[88:89] op_sel:[1,1] op_sel_hi:[0,1] neg_lo:[0,1]
	v_pk_fma_f32 v[90:91], v[180:181], v[88:89], v[20:21] op_sel_hi:[1,0,1]
	v_mov_b32_e32 v10, v165
	v_pk_mul_f32 v[20:21], v[180:181], v[90:91] op_sel:[1,1] op_sel_hi:[0,1] neg_lo:[0,1]
	v_pk_fma_f32 v[92:93], v[180:181], v[90:91], v[20:21] op_sel_hi:[1,0,1]
	v_pk_mul_f32 v[20:21], v[180:181], v[92:93] op_sel:[1,1] op_sel_hi:[0,1] neg_lo:[0,1]
	v_pk_fma_f32 v[94:95], v[180:181], v[92:93], v[20:21] op_sel_hi:[1,0,1]
	v_readlane_b32 s72, v251, 48
	v_pk_mul_f32 v[20:21], v[180:181], v[94:95] op_sel:[1,1] op_sel_hi:[0,1] neg_lo:[0,1]
	v_pk_fma_f32 v[96:97], v[180:181], v[94:95], v[20:21] op_sel_hi:[1,0,1]
	v_readlane_b32 s73, v251, 49
	v_pk_mul_f32 v[20:21], v[180:181], v[96:97] op_sel:[1,1] op_sel_hi:[0,1] neg_lo:[0,1]
	v_pk_fma_f32 v[98:99], v[180:181], v[96:97], v[20:21] op_sel_hi:[1,0,1]
	s_movk_i32 s10, 0xda00
	v_pk_mul_f32 v[20:21], v[180:181], v[98:99] op_sel:[1,1] op_sel_hi:[0,1] neg_lo:[0,1]
	v_pk_fma_f32 v[100:101], v[180:181], v[98:99], v[20:21] op_sel_hi:[1,0,1]
	s_mov_b32 s20, 0x3f61c598
	v_pk_mul_f32 v[20:21], v[180:181], v[100:101] op_sel:[1,1] op_sel_hi:[0,1] neg_lo:[0,1]
	v_pk_fma_f32 v[102:103], v[180:181], v[100:101], v[20:21] op_sel_hi:[1,0,1]
	s_mov_b32 s52, s95
	v_pk_mul_f32 v[20:21], v[180:181], v[102:103] op_sel:[1,1] op_sel_hi:[0,1] neg_lo:[0,1]
	v_pk_fma_f32 v[104:105], v[180:181], v[102:103], v[20:21] op_sel_hi:[1,0,1]
	s_mov_b32 s53, s94
	v_pk_mul_f32 v[20:21], v[180:181], v[104:105] op_sel:[1,1] op_sel_hi:[0,1] neg_lo:[0,1]
	v_pk_fma_f32 v[106:107], v[180:181], v[104:105], v[20:21] op_sel_hi:[1,0,1]
	s_mov_b32 s21, 0xbef15aea
	v_pk_mul_f32 v[20:21], v[180:181], v[106:107] op_sel:[1,1] op_sel_hi:[0,1] neg_lo:[0,1]
	v_pk_fma_f32 v[108:109], v[180:181], v[106:107], v[20:21] op_sel_hi:[1,0,1]
	s_mov_b32 s40, s47
	v_pk_mul_f32 v[20:21], v[180:181], v[108:109] op_sel:[1,1] op_sel_hi:[0,1] neg_lo:[0,1]
	v_pk_fma_f32 v[110:111], v[180:181], v[108:109], v[20:21] op_sel_hi:[1,0,1]
	s_mov_b32 s41, s42
	v_pk_mul_f32 v[20:21], v[180:181], v[110:111] op_sel:[1,1] op_sel_hi:[0,1] neg_lo:[0,1]
	v_pk_fma_f32 v[112:113], v[180:181], v[110:111], v[20:21] op_sel_hi:[1,0,1]
	s_mov_b32 s38, 0x3f3504f3
	v_pk_mul_f32 v[20:21], v[180:181], v[112:113] op_sel:[1,1] op_sel_hi:[0,1] neg_lo:[0,1]
	v_pk_fma_f32 v[20:21], v[180:181], v[112:113], v[20:21] op_sel_hi:[1,0,1]
	s_mov_b32 s39, 0xbf3504f3
	v_pk_mul_f32 v[114:115], v[180:181], v[20:21] op_sel:[1,1] op_sel_hi:[0,1] neg_lo:[0,1]
	v_pk_fma_f32 v[114:115], v[180:181], v[20:21], v[114:115] op_sel_hi:[1,0,1]
	v_mul_f32_e32 v18, v18, v20
	v_pk_mul_f32 v[116:117], v[180:181], v[114:115] op_sel:[1,1] op_sel_hi:[0,1] neg_lo:[0,1]
	v_pk_fma_f32 v[116:117], v[180:181], v[114:115], v[116:117] op_sel_hi:[1,0,1]
	v_fmac_f32_e32 v18, v19, v21
	v_pk_mul_f32 v[118:119], v[180:181], v[116:117] op_sel:[1,1] op_sel_hi:[0,1] neg_lo:[0,1]
	v_pk_fma_f32 v[118:119], v[180:181], v[116:117], v[118:119] op_sel_hi:[1,0,1]
	v_add_f32_e32 v17, v16, v18
	v_pk_mul_f32 v[120:121], v[180:181], v[118:119] op_sel:[1,1] op_sel_hi:[0,1] neg_lo:[0,1]
	v_pk_fma_f32 v[120:121], v[180:181], v[118:119], v[120:121] op_sel_hi:[1,0,1]
	s_mov_b32 s28, 0x3f226799
	v_pk_mul_f32 v[122:123], v[180:181], v[120:121] op_sel:[1,1] op_sel_hi:[0,1] neg_lo:[0,1]
	v_pk_fma_f32 v[122:123], v[180:181], v[120:121], v[122:123] op_sel_hi:[1,0,1]
	s_mov_b32 s29, 0xbf45e403
	v_pk_mul_f32 v[124:125], v[180:181], v[122:123] op_sel:[1,1] op_sel_hi:[0,1] neg_lo:[0,1]
	v_pk_fma_f32 v[124:125], v[180:181], v[122:123], v[124:125] op_sel_hi:[1,0,1]
	s_mov_b32 s82, 0x3f0e39da
	v_pk_mul_f32 v[126:127], v[180:181], v[124:125] op_sel:[1,1] op_sel_hi:[0,1] neg_lo:[0,1]
	v_pk_fma_f32 v[126:127], v[180:181], v[124:125], v[126:127] op_sel_hi:[1,0,1]
	s_mov_b32 s83, 0xbf54db31
	v_pk_mul_f32 v[128:129], v[180:181], v[126:127] op_sel:[1,1] op_sel_hi:[0,1] neg_lo:[0,1]
	v_pk_fma_f32 v[128:129], v[180:181], v[126:127], v[128:129] op_sel_hi:[1,0,1]
	s_mov_b32 s22, 0x3ef15aea
	v_pk_mul_f32 v[130:131], v[180:181], v[128:129] op_sel:[1,1] op_sel_hi:[0,1] neg_lo:[0,1]
	v_pk_fma_f32 v[130:131], v[180:181], v[128:129], v[130:131] op_sel_hi:[1,0,1]
	s_mov_b32 s23, 0xbf61c598
	v_pk_mul_f32 v[132:133], v[180:181], v[130:131] op_sel:[1,1] op_sel_hi:[0,1] neg_lo:[0,1]
	v_pk_fma_f32 v[132:133], v[180:181], v[130:131], v[132:133] op_sel_hi:[1,0,1]
	s_mov_b32 s18, 0x3ec3ef15
	v_pk_mul_f32 v[134:135], v[180:181], v[132:133] op_sel:[1,1] op_sel_hi:[0,1] neg_lo:[0,1]
	v_pk_fma_f32 v[134:135], v[180:181], v[132:133], v[134:135] op_sel_hi:[1,0,1]
	s_mov_b32 s19, 0xbf6c835e
	v_pk_mul_f32 v[136:137], v[180:181], v[134:135] op_sel:[1,1] op_sel_hi:[0,1] neg_lo:[0,1]
	v_pk_fma_f32 v[136:137], v[180:181], v[134:135], v[136:137] op_sel_hi:[1,0,1]
	s_mov_b32 s24, 0x3f54db31
	v_pk_mul_f32 v[138:139], v[180:181], v[136:137] op_sel:[1,1] op_sel_hi:[0,1] neg_lo:[0,1]
	v_pk_fma_f32 v[138:139], v[180:181], v[136:137], v[138:139] op_sel_hi:[1,0,1]
	s_mov_b32 s25, 0xbf0e39da
	v_pk_mul_f32 v[140:141], v[180:181], v[138:139] op_sel:[1,1] op_sel_hi:[0,1] neg_lo:[0,1]
	v_pk_fma_f32 v[140:141], v[180:181], v[138:139], v[140:141] op_sel_hi:[1,0,1]
	s_mov_b32 s74, 0x3f45e403
	v_pk_mul_f32 v[142:143], v[180:181], v[140:141] op_sel:[1,1] op_sel_hi:[0,1] neg_lo:[0,1]
	v_pk_fma_f32 v[22:23], v[180:181], v[140:141], v[142:143] op_sel_hi:[1,0,1]
	s_waitcnt lgkmcnt(0)
	v_pk_mul_f32 v[142:143], v[26:27], v[22:23] op_sel:[1,1] op_sel_hi:[0,1] neg_hi:[1,0]
	s_mov_b32 s75, 0xbf226799
	v_pk_fma_f32 v[26:27], v[26:27], v[22:23], v[142:143] op_sel_hi:[1,0,1]
	v_pk_mul_f32 v[22:23], v[28:29], v[140:141] op_sel:[1,1] op_sel_hi:[0,1] neg_hi:[1,0]
	s_mov_b32 s36, s77
	v_pk_fma_f32 v[28:29], v[28:29], v[140:141], v[22:23] op_sel_hi:[1,0,1]
	v_pk_mul_f32 v[22:23], v[32:33], v[138:139] op_sel:[1,1] op_sel_hi:[0,1] neg_hi:[1,0]
	s_mov_b32 s37, s43
	v_pk_fma_f32 v[32:33], v[32:33], v[138:139], v[22:23] op_sel_hi:[1,0,1]
	v_pk_mul_f32 v[22:23], v[34:35], v[136:137] op_sel:[1,1] op_sel_hi:[0,1] neg_hi:[1,0]
	s_mov_b32 s76, s43
	v_pk_fma_f32 v[34:35], v[34:35], v[136:137], v[22:23] op_sel_hi:[1,0,1]
	v_pk_mul_f32 v[22:23], v[36:37], v[134:135] op_sel:[1,1] op_sel_hi:[0,1] neg_hi:[1,0]
	s_mov_b32 s16, 0x3f6c835e
	v_pk_fma_f32 v[36:37], v[36:37], v[134:135], v[22:23] op_sel_hi:[1,0,1]
	v_pk_mul_f32 v[22:23], v[40:41], v[132:133] op_sel:[1,1] op_sel_hi:[0,1] neg_hi:[1,0]
	s_mov_b32 s17, 0xbec3ef15
	v_pk_fma_f32 v[40:41], v[40:41], v[132:133], v[22:23] op_sel_hi:[1,0,1]
	v_pk_mul_f32 v[22:23], v[42:43], v[130:131] op_sel:[1,1] op_sel_hi:[0,1] neg_hi:[1,0]
	s_mov_b32 s16, s19
	v_pk_fma_f32 v[42:43], v[42:43], v[130:131], v[22:23] op_sel_hi:[1,0,1]
	v_pk_mul_f32 v[22:23], v[82:83], v[128:129] op_sel:[1,1] op_sel_hi:[0,1] neg_hi:[1,0]
	s_mov_b32 s27, s29
	v_pk_fma_f32 v[22:23], v[82:83], v[128:129], v[22:23] op_sel_hi:[1,0,1]
	v_pk_mul_f32 v[82:83], v[48:49], v[126:127] op_sel:[1,1] op_sel_hi:[0,1] neg_hi:[1,0]
	s_mov_b32 s26, s75
	v_pk_fma_f32 v[48:49], v[48:49], v[126:127], v[82:83] op_sel_hi:[1,0,1]
	v_pk_mul_f32 v[82:83], v[52:53], v[124:125] op_sel:[1,1] op_sel_hi:[0,1] neg_hi:[1,0]
	s_mov_b32 s46, s42
	v_pk_fma_f32 v[52:53], v[52:53], v[124:125], v[82:83] op_sel_hi:[1,0,1]
	v_pk_mul_f32 v[82:83], v[56:57], v[122:123] op_sel:[1,1] op_sel_hi:[0,1] neg_hi:[1,0]
	v_mov_b32_e32 v124, v171
	v_pk_fma_f32 v[56:57], v[56:57], v[122:123], v[82:83] op_sel_hi:[1,0,1]
	v_pk_mul_f32 v[82:83], v[30:31], v[120:121] op_sel:[1,1] op_sel_hi:[0,1] neg_hi:[1,0]
	v_mov_b32_e32 v122, v169
	v_pk_fma_f32 v[30:31], v[30:31], v[120:121], v[82:83] op_sel_hi:[1,0,1]
	v_pk_mul_f32 v[82:83], v[38:39], v[118:119] op_sel:[1,1] op_sel_hi:[0,1] neg_hi:[1,0]
	v_mov_b32_e32 v120, v167
	v_pk_fma_f32 v[38:39], v[38:39], v[118:119], v[82:83] op_sel_hi:[1,0,1]
	v_pk_mul_f32 v[82:83], v[64:65], v[116:117] op_sel:[1,1] op_sel_hi:[0,1] neg_hi:[1,0]
	v_mov_b32_e32 v118, v165
	v_pk_fma_f32 v[64:65], v[64:65], v[116:117], v[82:83] op_sel_hi:[1,0,1]
	v_pk_mul_f32 v[82:83], v[66:67], v[114:115] op_sel:[1,1] op_sel_hi:[0,1] neg_hi:[1,0]
	s_nop 0
	v_pk_fma_f32 v[66:67], v[66:67], v[114:115], v[82:83] op_sel_hi:[1,0,1]
	v_pk_mul_f32 v[82:83], v[44:45], v[112:113] op_sel:[1,1] op_sel_hi:[0,1] neg_hi:[1,0]
	s_nop 0
	v_pk_fma_f32 v[44:45], v[44:45], v[112:113], v[82:83] op_sel_hi:[1,0,1]
	v_pk_mul_f32 v[82:83], v[46:47], v[110:111] op_sel:[1,1] op_sel_hi:[0,1] neg_hi:[1,0]
	s_nop 0
	v_pk_fma_f32 v[46:47], v[46:47], v[110:111], v[82:83] op_sel_hi:[1,0,1]
	v_pk_mul_f32 v[82:83], v[50:51], v[108:109] op_sel:[1,1] op_sel_hi:[0,1] neg_hi:[1,0]
	s_nop 0
	v_pk_fma_f32 v[50:51], v[50:51], v[108:109], v[82:83] op_sel_hi:[1,0,1]
	v_pk_mul_f32 v[82:83], v[54:55], v[106:107] op_sel:[1,1] op_sel_hi:[0,1] neg_hi:[1,0]
	s_nop 0
	v_pk_fma_f32 v[54:55], v[54:55], v[106:107], v[82:83] op_sel_hi:[1,0,1]
	v_pk_mul_f32 v[82:83], v[58:59], v[104:105] op_sel:[1,1] op_sel_hi:[0,1] neg_hi:[1,0]
	s_nop 0
	v_pk_fma_f32 v[58:59], v[58:59], v[104:105], v[82:83] op_sel_hi:[1,0,1]
	v_pk_mul_f32 v[82:83], v[60:61], v[102:103] op_sel:[1,1] op_sel_hi:[0,1] neg_hi:[1,0]
	s_nop 0
	v_pk_fma_f32 v[60:61], v[60:61], v[102:103], v[82:83] op_sel_hi:[1,0,1]
	v_pk_mul_f32 v[82:83], v[62:63], v[100:101] op_sel:[1,1] op_sel_hi:[0,1] neg_hi:[1,0]
	s_nop 0
	v_pk_fma_f32 v[62:63], v[62:63], v[100:101], v[82:83] op_sel_hi:[1,0,1]
	v_pk_mul_f32 v[82:83], v[24:25], v[98:99] op_sel:[1,1] op_sel_hi:[0,1] neg_hi:[1,0]
	s_nop 0
	v_pk_fma_f32 v[24:25], v[24:25], v[98:99], v[82:83] op_sel_hi:[1,0,1]
	v_pk_mul_f32 v[82:83], v[68:69], v[96:97] op_sel:[1,1] op_sel_hi:[0,1] neg_hi:[1,0]
	v_add_f32_e32 v22, v24, v22
	v_pk_fma_f32 v[68:69], v[68:69], v[96:97], v[82:83] op_sel_hi:[1,0,1]
	v_pk_mul_f32 v[82:83], v[70:71], v[94:95] op_sel:[1,1] op_sel_hi:[0,1] neg_hi:[1,0]
	v_add_f32_e32 v20, v17, v22
	v_pk_fma_f32 v[70:71], v[70:71], v[94:95], v[82:83] op_sel_hi:[1,0,1]
	v_pk_mul_f32 v[82:83], v[72:73], v[92:93] op_sel:[1,1] op_sel_hi:[0,1] neg_hi:[1,0]
	v_mov_b32_e32 v94, v171
	v_pk_fma_f32 v[72:73], v[72:73], v[92:93], v[82:83] op_sel_hi:[1,0,1]
	v_pk_mul_f32 v[82:83], v[74:75], v[90:91] op_sel:[1,1] op_sel_hi:[0,1] neg_hi:[1,0]
	v_mov_b32_e32 v92, v170
	v_pk_fma_f32 v[74:75], v[74:75], v[90:91], v[82:83] op_sel_hi:[1,0,1]
	v_pk_mul_f32 v[82:83], v[76:77], v[88:89] op_sel:[1,1] op_sel_hi:[0,1] neg_hi:[1,0]
	v_mov_b32_e32 v90, v169
	v_pk_fma_f32 v[76:77], v[76:77], v[88:89], v[82:83] op_sel_hi:[1,0,1]
	v_pk_mul_f32 v[82:83], v[78:79], v[86:87] op_sel:[1,1] op_sel_hi:[0,1] neg_hi:[1,0]
	v_mov_b32_e32 v88, v168
	v_pk_fma_f32 v[78:79], v[78:79], v[86:87], v[82:83] op_sel_hi:[1,0,1]
	v_pk_mul_f32 v[82:83], v[84:85], v[80:81] op_sel:[1,1] op_sel_hi:[1,0] neg_hi:[0,1]
	v_mov_b32_e32 v86, v167
	v_pk_fma_f32 v[80:81], v[80:81], v[84:85], v[82:83] op_sel_hi:[1,0,1]
	v_mov_b32_e32 v84, v166
	v_pk_add_f32 v[96:97], v[80:81], v[66:67]
	v_pk_add_f32 v[66:67], v[80:81], v[66:67] neg_lo:[0,1] neg_hi:[0,1]
	s_nop 0
	v_sub_f32_e32 v82, v25, v23
	v_pk_mul_f32 v[80:81], v[94:95], v[66:67] op_sel:[0,1] op_sel_hi:[0,0] neg_lo:[0,1]
	v_pk_fma_f32 v[80:81], v[10:11], v[66:67], v[80:81] op_sel_hi:[0,1,1]
	v_pk_add_f32 v[66:67], v[78:79], v[64:65]
	v_pk_add_f32 v[64:65], v[78:79], v[64:65] neg_lo:[0,1] neg_hi:[0,1]
	s_nop 0
	v_pk_mul_f32 v[78:79], v[92:93], v[64:65] op_sel:[0,1] op_sel_hi:[0,0] neg_lo:[0,1]
	v_pk_fma_f32 v[64:65], v[84:85], v[64:65], v[78:79] op_sel_hi:[0,1,1]
	v_pk_add_f32 v[78:79], v[76:77], v[38:39]
	v_pk_add_f32 v[38:39], v[76:77], v[38:39] neg_lo:[0,1] neg_hi:[0,1]
	s_barrier
	v_pk_mul_f32 v[76:77], v[90:91], v[38:39] op_sel:[0,1] op_sel_hi:[0,0] neg_lo:[0,1]
	v_pk_fma_f32 v[76:77], v[86:87], v[38:39], v[76:77] op_sel_hi:[0,1,1]
	v_pk_add_f32 v[38:39], v[74:75], v[30:31]
	v_pk_add_f32 v[30:31], v[74:75], v[30:31] neg_lo:[0,1] neg_hi:[0,1]
	s_nop 0
	v_pk_mul_f32 v[74:75], v[88:89], v[30:31] op_sel:[0,1] op_sel_hi:[0,0] neg_lo:[0,1]
	v_pk_fma_f32 v[30:31], v[88:89], v[30:31], v[74:75] op_sel_hi:[0,1,1]
	v_pk_add_f32 v[74:75], v[72:73], v[56:57]
	v_pk_add_f32 v[56:57], v[72:73], v[56:57] neg_lo:[0,1] neg_hi:[0,1]
	v_sub_f32_e32 v22, v17, v22
	v_pk_mul_f32 v[72:73], v[86:87], v[56:57] op_sel:[0,1] op_sel_hi:[0,0] neg_lo:[0,1]
	v_pk_fma_f32 v[72:73], v[90:91], v[56:57], v[72:73] op_sel_hi:[0,1,1]
	v_pk_add_f32 v[56:57], v[70:71], v[52:53]
	v_pk_add_f32 v[52:53], v[70:71], v[52:53] neg_lo:[0,1] neg_hi:[0,1]
	v_ashrrev_i32_e32 v15, 31, v14
	v_pk_mul_f32 v[70:71], v[84:85], v[52:53] op_sel:[0,1] op_sel_hi:[0,0] neg_lo:[0,1]
	v_pk_fma_f32 v[52:53], v[92:93], v[52:53], v[70:71] op_sel_hi:[0,1,1]
	v_pk_add_f32 v[70:71], v[68:69], v[48:49]
	v_pk_add_f32 v[48:49], v[68:69], v[48:49] neg_lo:[0,1] neg_hi:[0,1]
	v_lshl_add_u64 v[14:15], v[14:15], 2, s[72:73]
	v_pk_mul_f32 v[68:69], v[10:11], v[48:49] op_sel:[0,1] op_sel_hi:[0,0] neg_lo:[0,1]
	v_pk_fma_f32 v[98:99], v[94:95], v[48:49], v[68:69] op_sel_hi:[0,1,1]
	v_pk_add_f32 v[48:49], v[62:63], v[42:43]
	v_pk_add_f32 v[42:43], v[62:63], v[42:43] neg_lo:[0,1] neg_hi:[0,1]
	v_pk_add_f32 v[68:69], v[58:59], v[36:37]
	v_pk_mul_f32 v[62:63], v[10:11], v[42:43] op_sel:[0,1] op_sel_hi:[0,0] neg_lo:[0,1]
	v_pk_fma_f32 v[62:63], v[94:95], v[42:43], v[62:63] op_sel_hi:[0,1,1] neg_lo:[1,0,0] neg_hi:[1,0,0]
	v_pk_add_f32 v[42:43], v[60:61], v[40:41]
	v_pk_add_f32 v[40:41], v[60:61], v[40:41] neg_lo:[0,1] neg_hi:[0,1]
	v_pk_add_f32 v[36:37], v[58:59], v[36:37] neg_lo:[0,1] neg_hi:[0,1]
	v_pk_mul_f32 v[60:61], v[84:85], v[40:41] op_sel:[0,1] op_sel_hi:[0,0] neg_lo:[0,1]
	v_pk_fma_f32 v[60:61], v[92:93], v[40:41], v[60:61] op_sel_hi:[0,1,1] neg_lo:[1,0,0] neg_hi:[1,0,0]
	v_pk_mul_f32 v[40:41], v[86:87], v[36:37] op_sel:[0,1] op_sel_hi:[0,0] neg_lo:[0,1]
	v_pk_fma_f32 v[100:101], v[90:91], v[36:37], v[40:41] op_sel_hi:[0,1,1] neg_lo:[1,0,0] neg_hi:[1,0,0]
	v_pk_add_f32 v[40:41], v[54:55], v[34:35]
	v_pk_add_f32 v[34:35], v[54:55], v[34:35] neg_lo:[0,1] neg_hi:[0,1]
	v_add_f32_e32 v38, v38, v40
	v_pk_mul_f32 v[36:37], v[88:89], v[34:35] op_sel:[0,1] op_sel_hi:[0,0] neg_lo:[0,1]
	v_pk_fma_f32 v[34:35], v[88:89], v[34:35], v[36:37] op_sel_hi:[0,1,1] neg_lo:[1,0,0] neg_hi:[1,0,0]
	v_pk_add_f32 v[36:37], v[50:51], v[32:33]
	v_pk_add_f32 v[32:33], v[50:51], v[32:33] neg_lo:[0,1] neg_hi:[0,1]
	v_add_f32_e32 v30, v30, v34
	v_pk_mul_f32 v[50:51], v[90:91], v[32:33] op_sel:[0,1] op_sel_hi:[0,0] neg_lo:[0,1]
	v_pk_fma_f32 v[86:87], v[86:87], v[32:33], v[50:51] op_sel_hi:[0,1,1] neg_lo:[1,0,0] neg_hi:[1,0,0]
	v_pk_add_f32 v[32:33], v[46:47], v[28:29]
	v_pk_add_f32 v[28:29], v[46:47], v[28:29] neg_lo:[0,1] neg_hi:[0,1]
	v_pk_add_f32 v[50:51], v[44:45], v[26:27]
	v_pk_mul_f32 v[46:47], v[92:93], v[28:29] op_sel:[0,1] op_sel_hi:[0,0] neg_lo:[0,1]
	v_pk_add_f32 v[26:27], v[44:45], v[26:27] neg_lo:[0,1] neg_hi:[0,1]
	v_pk_fma_f32 v[46:47], v[84:85], v[28:29], v[46:47] op_sel_hi:[0,1,1] neg_lo:[1,0,0] neg_hi:[1,0,0]
	v_pk_mul_f32 v[28:29], v[94:95], v[26:27] op_sel:[0,1] op_sel_hi:[0,0] neg_lo:[0,1]
	v_pk_fma_f32 v[90:91], v[10:11], v[26:27], v[28:29] op_sel_hi:[0,1,1] neg_lo:[1,0,0] neg_hi:[1,0,0]
	v_pk_add_f32 v[28:29], v[96:97], v[48:49] neg_lo:[0,1] neg_hi:[0,1]
	v_pk_add_f32 v[26:27], v[96:97], v[48:49]
	v_pk_mul_f32 v[44:45], v[92:93], v[28:29] op_sel:[0,1] op_sel_hi:[0,0] neg_lo:[0,1]
	v_pk_fma_f32 v[94:95], v[84:85], v[28:29], v[44:45] op_sel_hi:[0,1,1]
	v_pk_add_f32 v[28:29], v[66:67], v[42:43] neg_lo:[0,1] neg_hi:[0,1]
	v_pk_add_f32 v[44:45], v[78:79], v[68:69] neg_lo:[0,1] neg_hi:[0,1]
	v_pk_add_f32 v[48:49], v[66:67], v[42:43]
	v_pk_mul_f32 v[42:43], v[88:89], v[28:29] op_sel:[0,1] op_sel_hi:[0,0] neg_lo:[0,1]
	v_pk_mul_f32 v[54:55], v[84:85], v[44:45] op_sel:[0,1] op_sel_hi:[0,0] neg_lo:[0,1]
	v_pk_fma_f32 v[28:29], v[88:89], v[28:29], v[42:43] op_sel_hi:[0,1,1]
	v_pk_add_f32 v[42:43], v[78:79], v[68:69]
	v_pk_fma_f32 v[68:69], v[92:93], v[44:45], v[54:55] op_sel_hi:[0,1,1]
	v_pk_add_f32 v[54:55], v[74:75], v[36:37]
	v_pk_add_f32 v[36:37], v[74:75], v[36:37] neg_lo:[0,1] neg_hi:[0,1]
	v_pk_add_f32 v[58:59], v[56:57], v[32:33]
	v_pk_mul_f32 v[44:45], v[84:85], v[36:37] op_sel:[0,1] op_sel_hi:[0,0] neg_lo:[0,1]
	v_pk_add_f32 v[32:33], v[56:57], v[32:33] neg_lo:[0,1] neg_hi:[0,1]
	v_pk_fma_f32 v[74:75], v[92:93], v[36:37], v[44:45] op_sel_hi:[0,1,1] neg_lo:[1,0,0] neg_hi:[1,0,0]
	v_pk_mul_f32 v[36:37], v[88:89], v[32:33] op_sel:[0,1] op_sel_hi:[0,0] neg_lo:[0,1]
	v_pk_fma_f32 v[44:45], v[88:89], v[32:33], v[36:37] op_sel_hi:[0,1,1] neg_lo:[1,0,0] neg_hi:[1,0,0]
	v_pk_add_f32 v[36:37], v[70:71], v[50:51] neg_lo:[0,1] neg_hi:[0,1]
	v_pk_add_f32 v[32:33], v[70:71], v[50:51]
	v_pk_mul_f32 v[50:51], v[92:93], v[36:37] op_sel:[0,1] op_sel_hi:[0,0] neg_lo:[0,1]
	v_pk_add_f32 v[66:67], v[26:27], v[54:55]
	v_pk_add_f32 v[26:27], v[26:27], v[54:55] neg_lo:[0,1] neg_hi:[0,1]
	v_pk_fma_f32 v[50:51], v[84:85], v[36:37], v[50:51] op_sel_hi:[0,1,1] neg_lo:[1,0,0] neg_hi:[1,0,0]
	v_pk_mul_f32 v[36:37], v[88:89], v[26:27] op_sel:[0,1] op_sel_hi:[0,0] neg_lo:[0,1]
	v_pk_add_f32 v[70:71], v[42:43], v[32:33]
	v_pk_add_f32 v[32:33], v[42:43], v[32:33] neg_lo:[0,1] neg_hi:[0,1]
	v_pk_fma_f32 v[26:27], v[88:89], v[26:27], v[36:37] op_sel_hi:[0,1,1]
	v_pk_mul_f32 v[36:37], v[88:89], v[32:33] op_sel:[0,1] op_sel_hi:[0,0] neg_lo:[0,1]
	v_pk_fma_f32 v[36:37], v[88:89], v[32:33], v[36:37] op_sel_hi:[0,1,1] neg_lo:[1,0,0] neg_hi:[1,0,0]
	v_pk_add_f32 v[32:33], v[94:95], v[74:75] neg_lo:[0,1] neg_hi:[0,1]
	v_pk_add_f32 v[56:57], v[68:69], v[50:51]
	v_pk_mul_f32 v[42:43], v[88:89], v[32:33] op_sel:[0,1] op_sel_hi:[0,0] neg_lo:[0,1]
	v_pk_fma_f32 v[32:33], v[88:89], v[32:33], v[42:43] op_sel_hi:[0,1,1]
	v_pk_add_f32 v[42:43], v[68:69], v[50:51] neg_lo:[0,1] neg_hi:[0,1]
	v_pk_add_f32 v[54:55], v[94:95], v[74:75]
	v_pk_mul_f32 v[50:51], v[88:89], v[42:43] op_sel:[0,1] op_sel_hi:[0,0] neg_lo:[0,1]
	v_pk_fma_f32 v[42:43], v[88:89], v[42:43], v[50:51] op_sel_hi:[0,1,1] neg_lo:[1,0,0] neg_hi:[1,0,0]
	v_pk_add_f32 v[50:51], v[80:81], v[62:63] neg_lo:[0,1] neg_hi:[0,1]
	v_pk_add_f32 v[74:75], v[80:81], v[62:63]
	v_pk_mul_f32 v[62:63], v[92:93], v[50:51] op_sel:[0,1] op_sel_hi:[0,0] neg_lo:[0,1]
	v_pk_fma_f32 v[94:95], v[84:85], v[50:51], v[62:63] op_sel_hi:[0,1,1]
	v_pk_add_f32 v[50:51], v[64:65], v[60:61] neg_lo:[0,1] neg_hi:[0,1]
	v_pk_add_f32 v[68:69], v[64:65], v[60:61]
	v_pk_mul_f32 v[60:61], v[88:89], v[50:51] op_sel:[0,1] op_sel_hi:[0,0] neg_lo:[0,1]
	v_pk_fma_f32 v[50:51], v[88:89], v[50:51], v[60:61] op_sel_hi:[0,1,1]
	v_pk_add_f32 v[60:61], v[76:77], v[100:101] neg_lo:[0,1] neg_hi:[0,1]
	v_pk_add_f32 v[64:65], v[76:77], v[100:101]
	v_pk_mul_f32 v[62:63], v[84:85], v[60:61] op_sel:[0,1] op_sel_hi:[0,0] neg_lo:[0,1]
	v_pk_fma_f32 v[96:97], v[92:93], v[60:61], v[62:63] op_sel_hi:[0,1,1]
	v_pk_add_f32 v[60:61], v[72:73], v[86:87] neg_lo:[0,1] neg_hi:[0,1]
	v_pk_add_f32 v[76:77], v[52:53], v[46:47]
	v_pk_add_f32 v[46:47], v[52:53], v[46:47] neg_lo:[0,1] neg_hi:[0,1]
	v_pk_add_f32 v[62:63], v[72:73], v[86:87]
	v_pk_mul_f32 v[72:73], v[84:85], v[60:61] op_sel:[0,1] op_sel_hi:[0,0] neg_lo:[0,1]
	v_pk_mul_f32 v[52:53], v[88:89], v[46:47] op_sel:[0,1] op_sel_hi:[0,0] neg_lo:[0,1]
	v_pk_fma_f32 v[86:87], v[92:93], v[60:61], v[72:73] op_sel_hi:[0,1,1] neg_lo:[1,0,0] neg_hi:[1,0,0]
	v_pk_fma_f32 v[60:61], v[88:89], v[46:47], v[52:53] op_sel_hi:[0,1,1] neg_lo:[1,0,0] neg_hi:[1,0,0]
	v_pk_add_f32 v[46:47], v[98:99], v[90:91]
	v_pk_add_f32 v[52:53], v[98:99], v[90:91] neg_lo:[0,1] neg_hi:[0,1]
	v_pk_add_f32 v[80:81], v[64:65], v[46:47]
	v_pk_add_f32 v[46:47], v[64:65], v[46:47] neg_lo:[0,1] neg_hi:[0,1]
	s_nop 0
	v_pk_mul_f32 v[64:65], v[88:89], v[46:47] op_sel:[0,1] op_sel_hi:[0,0] neg_lo:[0,1]
	v_pk_fma_f32 v[64:65], v[88:89], v[46:47], v[64:65] op_sel_hi:[0,1,1] neg_lo:[1,0,0] neg_hi:[1,0,0]
	v_pk_add_f32 v[46:47], v[94:95], v[86:87] neg_lo:[0,1] neg_hi:[0,1]
	v_pk_mul_f32 v[72:73], v[92:93], v[52:53] op_sel:[0,1] op_sel_hi:[0,0] neg_lo:[0,1]
	v_pk_add_f32 v[78:79], v[74:75], v[62:63]
	v_pk_add_f32 v[62:63], v[74:75], v[62:63] neg_lo:[0,1] neg_hi:[0,1]
	v_pk_fma_f32 v[52:53], v[84:85], v[52:53], v[72:73] op_sel_hi:[0,1,1] neg_lo:[1,0,0] neg_hi:[1,0,0]
	v_pk_mul_f32 v[74:75], v[88:89], v[46:47] op_sel:[0,1] op_sel_hi:[0,0] neg_lo:[0,1]
	v_pk_fma_f32 v[46:47], v[88:89], v[46:47], v[74:75] op_sel_hi:[0,1,1]
	v_pk_add_f32 v[74:75], v[96:97], v[52:53]
	v_pk_add_f32 v[52:53], v[96:97], v[52:53] neg_lo:[0,1] neg_hi:[0,1]
	v_sub_f32_e32 v34, v16, v18
	v_pk_mul_f32 v[84:85], v[88:89], v[52:53] op_sel:[0,1] op_sel_hi:[0,0] neg_lo:[0,1]
	v_sub_f32_e32 v25, v33, v43
	v_sub_f32_e32 v43, v31, v35
	v_sub_f32_e32 v35, v51, v61
	v_pk_fma_f32 v[52:53], v[88:89], v[52:53], v[84:85] op_sel_hi:[0,1,1] neg_lo:[1,0,0] neg_hi:[1,0,0]
	v_sub_f32_e32 v51, v34, v82
	v_sub_f32_e32 v13, v49, v59
	v_sub_f32_e32 v10, v47, v53
	v_add_f32_e32 v49, v68, v76
	v_add_f32_e32 v53, v51, v30
	v_sub_f32_e32 v23, v27, v37
	v_sub_f32_e32 v27, v55, v57
	v_add_f32_e32 v40, v78, v80
	v_add_f32_e32 v55, v53, v49
	v_add_f32_e32 v16, v55, v40
	v_sub_f32_e32 v41, v39, v41
	v_add_f32_e32 v48, v48, v58
	v_add_f32_e32 v21, v20, v38
	global_store_dword v[14:15], v16, off offset:2048
	v_add_co_u32_e32 v16, vcc, s85, v14
	v_add_f32_e32 v47, v66, v70
	v_add_f32_e32 v24, v21, v48
	v_add_f32_e32 v28, v28, v44
	v_sub_f32_e32 v44, v22, v41
	v_addc_co_u32_e32 v17, vcc, 0, v15, vcc
	v_pk_mul_f32 v[72:73], v[88:89], v[62:63] op_sel:[0,1] op_sel_hi:[0,0] neg_lo:[0,1]
	v_add_f32_e32 v19, v24, v47
	v_add_f32_e32 v54, v54, v56
	v_add_f32_e32 v56, v44, v28
	v_add_co_u32_e32 v18, vcc, s84, v14
	v_add_f32_e32 v34, v34, v82
	v_pk_fma_f32 v[62:63], v[88:89], v[62:63], v[72:73] op_sel_hi:[0,1,1]
	v_pk_add_f32 v[72:73], v[94:95], v[86:87]
	global_store_dword v[14:15], v19, off
	v_add_f32_e32 v57, v56, v54
	v_addc_co_u32_e32 v19, vcc, 0, v15, vcc
	v_add_f32_e32 v50, v50, v60
	v_sub_f32_e32 v58, v34, v43
	global_store_dword v[18:19], v57, off offset:-4096
	v_add_f32_e32 v57, v72, v74
	v_add_f32_e32 v59, v58, v50
	v_sub_f32_e32 v20, v20, v38
	v_sub_f32_e32 v37, v29, v45
	v_sub_f32_e32 v45, v69, v77
	v_add_f32_e32 v60, v59, v57
	v_add_f32_e32 v26, v26, v36
	v_sub_f32_e32 v36, v20, v13
	v_sub_f32_e32 v30, v51, v30
	global_store_dword v[16:17], v60, off offset:2048
	v_add_f32_e32 v16, v36, v26
	v_add_f32_e32 v38, v62, v64
	v_sub_f32_e32 v51, v30, v45
	global_store_dword v[18:19], v16, off
	v_add_f32_e32 v16, v51, v38
	global_store_dword v[18:19], v16, off offset:2048
	v_add_co_u32_e32 v16, vcc, s61, v14
	v_add_f32_e32 v22, v22, v41
	s_nop 0
	v_addc_co_u32_e32 v17, vcc, 0, v15, vcc
	v_add_f32_e32 v32, v32, v42
	v_sub_f32_e32 v41, v22, v37
	v_add_co_u32_e32 v18, vcc, s45, v14
	v_add_f32_e32 v42, v41, v32
	s_nop 0
	v_addc_co_u32_e32 v19, vcc, 0, v15, vcc
	v_add_f32_e32 v34, v34, v43
	global_store_dword v[18:19], v42, off offset:-4096
	v_add_f32_e32 v42, v46, v52
	v_sub_f32_e32 v43, v34, v35
	v_sub_f32_e32 v39, v67, v71
	v_add_f32_e32 v46, v43, v42
	v_sub_f32_e32 v21, v21, v48
	v_sub_f32_e32 v33, v79, v81
	global_store_dword v[16:17], v46, off offset:2048
	v_sub_f32_e32 v16, v21, v39
	v_sub_f32_e32 v46, v53, v49
	global_store_dword v[18:19], v16, off
	v_sub_f32_e32 v16, v46, v33
	global_store_dword v[18:19], v16, off offset:2048
	v_add_co_u32_e32 v16, vcc, s86, v14
	v_sub_f32_e32 v28, v44, v28
	s_nop 0
	v_addc_co_u32_e32 v17, vcc, 0, v15, vcc
	v_add_co_u32_e32 v18, vcc, s88, v14
	v_sub_f32_e32 v44, v28, v27
	s_nop 0
	v_addc_co_u32_e32 v19, vcc, 0, v15, vcc
	v_sub_f32_e32 v31, v73, v75
	global_store_dword v[18:19], v44, off offset:-4096
	v_sub_f32_e32 v44, v58, v50
	v_sub_f32_e32 v48, v44, v31
	v_add_f32_e32 v20, v20, v13
	v_sub_f32_e32 v29, v63, v65
	global_store_dword v[16:17], v48, off offset:2048
	v_sub_f32_e32 v13, v20, v23
	v_add_f32_e32 v30, v30, v45
	v_add_co_u32_e32 v16, vcc, s90, v14
	global_store_dword v[18:19], v13, off
	v_sub_f32_e32 v13, v30, v29
	v_addc_co_u32_e32 v17, vcc, 0, v15, vcc
	global_store_dword v[18:19], v13, off offset:2048
	v_add_f32_e32 v22, v22, v37
	v_add_co_u32_e32 v18, vcc, s8, v14
	v_sub_f32_e32 v13, v22, v25
	s_nop 0
	v_addc_co_u32_e32 v19, vcc, 0, v15, vcc
	global_store_dword v[18:19], v13, off offset:-4096
	v_add_f32_e32 v13, v34, v35
	v_sub_f32_e32 v34, v13, v10
	global_store_dword v[16:17], v34, off offset:2048
	v_sub_f32_e32 v16, v24, v47
	global_store_dword v[18:19], v16, off
	v_sub_f32_e32 v16, v55, v40
	global_store_dword v[18:19], v16, off offset:2048
	v_add_co_u32_e32 v16, vcc, s9, v14
	v_sub_f32_e32 v24, v56, v54
	s_nop 0
	v_addc_co_u32_e32 v17, vcc, 0, v15, vcc
	v_add_co_u32_e32 v18, vcc, s7, v14
	v_add_f32_e32 v10, v13, v10
	s_nop 0
	v_addc_co_u32_e32 v19, vcc, 0, v15, vcc
	global_store_dword v[18:19], v24, off offset:-4096
	v_sub_f32_e32 v24, v59, v57
	global_store_dword v[16:17], v24, off offset:2048
	v_sub_f32_e32 v16, v36, v26
	global_store_dword v[18:19], v16, off
	v_sub_f32_e32 v16, v51, v38
	global_store_dword v[18:19], v16, off offset:2048
	v_add_co_u32_e32 v16, vcc, s5, v14
	v_sub_f32_e32 v24, v41, v32
	s_nop 0
	v_addc_co_u32_e32 v17, vcc, 0, v15, vcc
	v_add_co_u32_e32 v18, vcc, s6, v14
	s_nop 1
	v_addc_co_u32_e32 v19, vcc, 0, v15, vcc
	global_store_dword v[18:19], v24, off offset:-4096
	v_sub_f32_e32 v24, v43, v42
	global_store_dword v[16:17], v24, off offset:2048
	v_add_f32_e32 v16, v21, v39
	global_store_dword v[18:19], v16, off
	v_add_f32_e32 v16, v46, v33
	global_store_dword v[18:19], v16, off offset:2048
	v_add_co_u32_e32 v16, vcc, s4, v14
	v_add_f32_e32 v21, v28, v27
	s_nop 0
	v_addc_co_u32_e32 v17, vcc, 0, v15, vcc
	v_add_co_u32_e32 v18, vcc, s1, v14
	s_nop 1
	v_addc_co_u32_e32 v19, vcc, 0, v15, vcc
	global_store_dword v[18:19], v21, off offset:-4096
	v_add_f32_e32 v21, v44, v31
	global_store_dword v[16:17], v21, off offset:2048
	v_add_f32_e32 v16, v20, v23
	global_store_dword v[18:19], v16, off
	v_add_f32_e32 v16, v30, v29
	v_add_co_u32_e32 v14, vcc, s0, v14
	global_store_dword v[18:19], v16, off offset:2048
	v_add_f32_e32 v16, v22, v25
	v_addc_co_u32_e32 v15, vcc, 0, v15, vcc
	global_store_dword v[14:15], v16, off
	global_store_dword v[14:15], v10, off offset:2048
	v_mov_b32_e32 v10, v184
	v_mov_b32_e32 v14, v185
	v_mov_b32_e32 v18, v1
	s_movk_i32 s0, 0xfe00
	v_sub_u32_e32 v13, 0x4000, v18
	v_cmp_eq_u32_e32 vcc, 0, v18
	v_cmp_eq_u32_e64 s[0:1], s0, v18
	v_cmp_eq_u32_e64 s[4:5], s50, v18
	v_cndmask_b32_e64 v20, v13, 0, vcc
	v_sub_u32_e32 v13, 0x3e00, v18
	v_cndmask_b32_e64 v22, v13, 0, s[0:1]
	v_sub_u32_e32 v13, 0x3c00, v18
	v_ashrrev_i32_e32 v21, 31, v20
	v_ashrrev_i32_e32 v23, 31, v22
	v_cndmask_b32_e64 v24, v13, 0, s[4:5]
	v_lshl_add_u64 v[20:21], v[20:21], 1, s[2:3]
	v_lshl_add_u64 v[22:23], v[22:23], 1, s[2:3]
	v_ashrrev_i32_e32 v25, 31, v24
	v_sub_u32_e32 v13, 0x3a00, v18
	v_cmp_eq_u32_e64 s[6:7], s51, v18
	v_lshl_add_u64 v[24:25], v[24:25], 1, s[2:3]
	global_load_ushort v15, v[20:21], off
	s_nop 0
	global_load_ushort v22, v[22:23], off
	s_nop 0
	global_load_ushort v23, v[24:25], off
	v_cndmask_b32_e64 v20, v13, 0, s[6:7]
	v_ashrrev_i32_e32 v21, 31, v20
	v_ashrrev_i32_e32 v19, 31, v18
	v_lshl_add_u64 v[20:21], v[20:21], 1, s[2:3]
	v_lshl_add_u64 v[16:17], v[18:19], 1, s[78:79]
	global_load_ushort v20, v[20:21], off
	s_nop 0
	global_load_ushort v13, v[16:17], off offset:3072
	v_sub_u32_e32 v24, 0x3800, v18
	v_sub_u32_e32 v26, 0x3600, v18
	v_sub_u32_e32 v28, 0x3400, v18
	v_sub_u32_e32 v32, 0x3200, v18
	v_cmp_eq_u32_e64 s[8:9], s60, v18
	v_cmp_eq_u32_e64 s[10:11], s10, v18
	s_mov_b32 s78, s69
	s_mov_b32 s79, s68
	s_mov_b32 s50, s21
	s_mov_b32 s51, s20
	s_mov_b32 s60, s25
	s_waitcnt vmcnt(4)
	v_lshlrev_b32_e32 v15, 16, v15
	v_cndmask_b32_e64 v19, -v15, v15, vcc
	s_waitcnt vmcnt(3)
	v_lshlrev_b32_e32 v15, 16, v22
	v_add_co_u32_e32 v22, vcc, s85, v16
	v_cndmask_b32_e64 v31, -v15, v15, s[0:1]
	s_waitcnt vmcnt(2)
	v_lshlrev_b32_e32 v15, 16, v23
	v_addc_co_u32_e32 v23, vcc, 0, v17, vcc
	v_cndmask_b32_e64 v30, -v15, v15, s[4:5]
	s_waitcnt vmcnt(1)
	v_lshlrev_b32_e32 v15, 16, v20
	v_add_co_u32_e32 v20, vcc, s84, v16
	v_cndmask_b32_e64 v15, -v15, v15, s[6:7]
	s_nop 0
	v_addc_co_u32_e32 v21, vcc, 0, v17, vcc
	v_cmp_eq_u32_e64 s[6:7], s56, v18
	v_cmp_eq_u32_e64 s[4:5], s57, v18
	v_cmp_eq_u32_e64 s[0:1], s58, v18
	v_cndmask_b32_e64 v24, v24, 0, s[6:7]
	v_cndmask_b32_e64 v26, v26, 0, s[4:5]
	v_cndmask_b32_e64 v28, v28, 0, s[0:1]
	v_cmp_eq_u32_e32 vcc, s59, v18
	v_ashrrev_i32_e32 v25, 31, v24
	v_ashrrev_i32_e32 v27, 31, v26
	v_ashrrev_i32_e32 v29, 31, v28
	v_cndmask_b32_e64 v32, v32, 0, vcc
	v_lshl_add_u64 v[24:25], v[24:25], 1, s[2:3]
	v_lshl_add_u64 v[26:27], v[26:27], 1, s[2:3]
	v_lshl_add_u64 v[28:29], v[28:29], 1, s[2:3]
	v_ashrrev_i32_e32 v33, 31, v32
	v_lshl_add_u64 v[32:33], v[32:33], 1, s[2:3]
	global_load_ushort v34, v[24:25], off
	s_nop 0
	global_load_ushort v26, v[26:27], off
	s_nop 0
	global_load_ushort v27, v[28:29], off
	s_nop 0
	global_load_ushort v28, v[32:33], off
	v_sub_u32_e32 v24, 0x3000, v18
	v_cndmask_b32_e64 v24, v24, 0, s[8:9]
	v_ashrrev_i32_e32 v25, 31, v24
	v_lshl_add_u64 v[24:25], v[24:25], 1, s[2:3]
	global_load_ushort v24, v[24:25], off
	s_nop 0
	global_load_ushort v33, v[22:23], off offset:3072
	s_waitcnt vmcnt(6)
	v_lshlrev_b32_e32 v13, 16, v13
	s_mov_b32 s56, s39
	s_mov_b32 s57, s38
	s_mov_b32 s58, s19
	s_mov_b32 s59, s18
	s_waitcnt vmcnt(5)
	v_lshlrev_b32_e32 v25, 16, v34
	v_cndmask_b32_e64 v32, -v25, v25, s[6:7]
	s_waitcnt vmcnt(4)
	v_lshlrev_b32_e32 v25, 16, v26
	v_cndmask_b32_e64 v36, -v25, v25, s[4:5]
	s_waitcnt vmcnt(3)
	v_lshlrev_b32_e32 v25, 16, v27
	v_cndmask_b32_e64 v37, -v25, v25, s[0:1]
	v_add_co_u32_e64 v26, s[0:1], s61, v16
	s_waitcnt vmcnt(2)
	v_lshlrev_b32_e32 v25, 16, v28
	s_waitcnt vmcnt(1)
	v_lshlrev_b32_e32 v24, 16, v24
	v_addc_co_u32_e64 v27, s[0:1], 0, v17, s[0:1]
	v_cndmask_b32_e64 v35, -v25, v25, vcc
	v_cndmask_b32_e64 v34, -v24, v24, s[8:9]
	v_sub_u32_e32 v24, 0x2e00, v18
	v_cmp_eq_u32_e32 vcc, s62, v18
	v_sub_u32_e32 v28, 0x2c00, v18
	v_cmp_eq_u32_e64 s[0:1], s63, v18
	v_cndmask_b32_e64 v24, v24, 0, vcc
	v_ashrrev_i32_e32 v25, 31, v24
	v_cndmask_b32_e64 v28, v28, 0, s[0:1]
	v_ashrrev_i32_e32 v29, 31, v28
	v_lshl_add_u64 v[24:25], v[24:25], 1, s[2:3]
	v_lshl_add_u64 v[28:29], v[28:29], 1, s[2:3]
	global_load_ushort v38, v[24:25], off
	s_nop 0
	global_load_ushort v28, v[28:29], off
	v_sub_u32_e32 v24, 0x2a00, v18
	v_cmp_eq_u32_e64 s[4:5], s64, v18
	v_cmp_eq_u32_e64 s[6:7], s65, v18
	s_mov_b32 s62, s29
	v_cndmask_b32_e64 v24, v24, 0, s[4:5]
	v_ashrrev_i32_e32 v25, 31, v24
	v_lshl_add_u64 v[24:25], v[24:25], 1, s[2:3]
	global_load_ushort v29, v[24:25], off
	v_sub_u32_e32 v24, 0x2800, v18
	v_cndmask_b32_e64 v24, v24, 0, s[6:7]
	v_ashrrev_i32_e32 v25, 31, v24
	v_lshl_add_u64 v[24:25], v[24:25], 1, s[2:3]
	global_load_ushort v41, v[26:27], off offset:1024
	global_load_ushort v40, v[26:27], off offset:2048
	global_load_ushort v39, v[26:27], off offset:3072
	global_load_ushort v42, v[24:25], off
	v_sub_u32_e32 v26, 0x2600, v18
	s_mov_b32 s63, s28
	s_mov_b32 s61, s24
	s_waitcnt vmcnt(6)
	v_lshlrev_b32_e32 v24, 16, v38
	v_cndmask_b32_e64 v45, -v24, v24, vcc
	s_waitcnt vmcnt(5)
	v_lshlrev_b32_e32 v24, 16, v28
	v_cndmask_b32_e64 v44, -v24, v24, s[0:1]
	s_movk_i32 s0, 0xe600
	v_sub_u32_e32 v38, 0x2200, v18
	s_waitcnt vmcnt(4)
	v_lshlrev_b32_e32 v24, 16, v29
	v_cndmask_b32_e64 v43, -v24, v24, s[4:5]
	v_add_co_u32_e32 v24, vcc, s45, v16
	s_nop 1
	v_addc_co_u32_e32 v25, vcc, 0, v17, vcc
	v_cmp_eq_u32_e32 vcc, s0, v18
	s_movk_i32 s0, 0xe400
	s_nop 0
	v_cndmask_b32_e64 v26, v26, 0, vcc
	v_ashrrev_i32_e32 v27, 31, v26
	v_lshl_add_u64 v[26:27], v[26:27], 1, s[2:3]
	global_load_ushort v26, v[26:27], off
	s_waitcnt vmcnt(1)
	v_lshlrev_b32_e32 v27, 16, v42
	v_cndmask_b32_e64 v49, -v27, v27, s[6:7]
	s_waitcnt vmcnt(0)
	v_lshlrev_b32_e32 v26, 16, v26
	v_cndmask_b32_e64 v50, -v26, v26, vcc
	v_cmp_eq_u32_e32 vcc, s0, v18
	v_add_co_u32_e64 v28, s[0:1], s86, v16
	v_sub_u32_e32 v26, 0x2400, v18
	s_nop 0
	v_addc_co_u32_e64 v29, s[0:1], 0, v17, s[0:1]
	s_movk_i32 s0, 0xe200
	s_nop 0
	v_cmp_eq_u32_e64 s[8:9], s0, v18
	s_movk_i32 s0, 0xe000
	v_cmp_eq_u32_e64 s[6:7], s0, v18
	v_cndmask_b32_e64 v46, v38, 0, s[8:9]
	v_sub_u32_e32 v38, 0x2000, v18
	s_movk_i32 s0, 0xde00
	v_cndmask_b32_e64 v52, v38, 0, s[6:7]
	v_sub_u32_e32 v38, 0x1e00, v18
	v_cmp_eq_u32_e64 s[4:5], s0, v18
	s_movk_i32 s0, 0xdc00
	v_cndmask_b32_e64 v26, v26, 0, vcc
	v_cndmask_b32_e64 v54, v38, 0, s[4:5]
	v_sub_u32_e32 v38, 0x1c00, v18
	v_cmp_eq_u32_e64 s[0:1], s0, v18
	v_ashrrev_i32_e32 v27, 31, v26
	v_ashrrev_i32_e32 v47, 31, v46
	v_cndmask_b32_e64 v56, v38, 0, s[0:1]
	v_lshl_add_u64 v[26:27], v[26:27], 1, s[2:3]
	v_lshl_add_u64 v[46:47], v[46:47], 1, s[2:3]
	v_ashrrev_i32_e32 v53, 31, v52
	v_ashrrev_i32_e32 v55, 31, v54
	v_ashrrev_i32_e32 v57, 31, v56
	v_lshl_add_u64 v[52:53], v[52:53], 1, s[2:3]
	v_lshl_add_u64 v[54:55], v[54:55], 1, s[2:3]
	v_lshl_add_u64 v[56:57], v[56:57], 1, s[2:3]
	global_load_ushort v38, v[26:27], off
	global_load_ushort v42, v[46:47], off
	s_nop 0
	global_load_ushort v46, v[52:53], off
	global_load_ushort v47, v[54:55], off
	global_load_ushort v48, v[56:57], off
	v_sub_u32_e32 v26, 0x1a00, v18
	v_cndmask_b32_e64 v26, v26, 0, s[10:11]
	v_ashrrev_i32_e32 v27, 31, v26
	v_lshl_add_u64 v[26:27], v[26:27], 1, s[2:3]
	global_load_ushort v26, v[26:27], off
	s_nop 0
	global_load_ushort v53, v[28:29], off offset:1024
	global_load_ushort v51, v[28:29], off offset:2048
	s_waitcnt vmcnt(7)
	v_lshlrev_b32_e32 v27, 16, v38
	v_cndmask_b32_e64 v61, -v27, v27, vcc
	s_waitcnt vmcnt(6)
	v_lshlrev_b32_e32 v27, 16, v42
	v_cndmask_b32_e64 v63, -v27, v27, s[8:9]
	s_waitcnt vmcnt(5)
	v_lshlrev_b32_e32 v27, 16, v46
	v_cndmask_b32_e64 v90, -v27, v27, s[6:7]
	s_waitcnt vmcnt(4)
	v_lshlrev_b32_e32 v27, 16, v47
	v_cndmask_b32_e64 v59, -v27, v27, s[4:5]
	s_waitcnt vmcnt(3)
	v_lshlrev_b32_e32 v27, 16, v48
	v_cndmask_b32_e64 v57, -v27, v27, s[0:1]
	s_movk_i32 s0, 0xd800
	v_sub_u32_e32 v38, 0x1800, v18
	v_cmp_eq_u32_e64 s[8:9], s0, v18
	s_movk_i32 s0, 0xd600
	s_waitcnt vmcnt(2)
	v_lshlrev_b32_e32 v26, 16, v26
	v_cndmask_b32_e64 v46, v38, 0, s[8:9]
	v_sub_u32_e32 v38, 0x1600, v18
	v_cmp_eq_u32_e64 s[6:7], s0, v18
	s_movk_i32 s0, 0xd400
	v_cndmask_b32_e64 v55, -v26, v26, s[10:11]
	v_add_co_u32_e32 v26, vcc, s88, v16
	v_cndmask_b32_e64 v64, v38, 0, s[6:7]
	v_sub_u32_e32 v38, 0x1400, v18
	v_cmp_eq_u32_e64 s[4:5], s0, v18
	s_movk_i32 s0, 0xd200
	v_addc_co_u32_e32 v27, vcc, 0, v17, vcc
	v_cndmask_b32_e64 v66, v38, 0, s[4:5]
	v_sub_u32_e32 v38, 0x1200, v18
	v_cmp_eq_u32_e64 s[0:1], s0, v18
	s_movk_i32 s10, 0xd000
	v_cmp_eq_u32_e32 vcc, s10, v18
	v_cndmask_b32_e64 v68, v38, 0, s[0:1]
	v_sub_u32_e32 v38, 0x1000, v18
	v_ashrrev_i32_e32 v47, 31, v46
	v_cndmask_b32_e64 v70, v38, 0, vcc
	v_lshl_add_u64 v[46:47], v[46:47], 1, s[2:3]
	v_ashrrev_i32_e32 v65, 31, v64
	v_ashrrev_i32_e32 v67, 31, v66
	v_ashrrev_i32_e32 v69, 31, v68
	v_ashrrev_i32_e32 v71, 31, v70
	s_movk_i32 s10, 0xce00
	v_lshl_add_u64 v[64:65], v[64:65], 1, s[2:3]
	v_lshl_add_u64 v[66:67], v[66:67], 1, s[2:3]
	v_lshl_add_u64 v[68:69], v[68:69], 1, s[2:3]
	v_lshl_add_u64 v[70:71], v[70:71], 1, s[2:3]
	global_load_ushort v38, v[46:47], off
	global_load_ushort v42, v[64:65], off
	global_load_ushort v48, v[66:67], off
	global_load_ushort v52, v[68:69], off
	global_load_ushort v54, v[70:71], off
	v_sub_u32_e32 v46, 0xe00, v18
	v_cmp_eq_u32_e64 s[12:13], s10, v18
	s_movk_i32 s10, 0xcc00
	v_cmp_eq_u32_e64 s[10:11], s10, v18
	v_cndmask_b32_e64 v46, v46, 0, s[12:13]
	v_ashrrev_i32_e32 v47, 31, v46
	v_lshl_add_u64 v[46:47], v[46:47], 1, s[2:3]
	global_load_ushort v56, v[46:47], off
	v_sub_u32_e32 v46, 0xc00, v18
	v_cndmask_b32_e64 v46, v46, 0, s[10:11]
	v_ashrrev_i32_e32 v47, 31, v46
	v_lshl_add_u64 v[46:47], v[46:47], 1, s[2:3]
	global_load_ushort v46, v[46:47], off
	s_nop 0
	global_load_ushort v91, v[28:29], off offset:3072
	s_waitcnt vmcnt(7)
	v_lshlrev_b32_e32 v28, 16, v38
	v_cndmask_b32_e64 v97, -v28, v28, s[8:9]
	s_waitcnt vmcnt(6)
	v_lshlrev_b32_e32 v28, 16, v42
	v_cndmask_b32_e64 v96, -v28, v28, s[6:7]
	s_waitcnt vmcnt(5)
	v_lshlrev_b32_e32 v28, 16, v48
	v_cndmask_b32_e64 v94, -v28, v28, s[4:5]
	s_waitcnt vmcnt(4)
	v_lshlrev_b32_e32 v28, 16, v52
	v_cndmask_b32_e64 v93, -v28, v28, s[0:1]
	s_waitcnt vmcnt(3)
	v_lshlrev_b32_e32 v28, 16, v54
	v_cndmask_b32_e64 v92, -v28, v28, vcc
	s_movk_i32 s0, 0xca00
	v_cmp_eq_u32_e64 s[0:1], s0, v18
	s_waitcnt vmcnt(2)
	v_lshlrev_b32_e32 v28, 16, v56
	v_cndmask_b32_e64 v95, -v28, v28, s[12:13]
	v_sub_u32_e32 v28, 0xa00, v18
	v_cndmask_b32_e64 v28, v28, 0, s[0:1]
	v_ashrrev_i32_e32 v29, 31, v28
	v_lshl_add_u64 v[28:29], v[28:29], 1, s[2:3]
	global_load_ushort v38, v[28:29], off
	s_waitcnt vmcnt(2)
	v_lshlrev_b32_e32 v28, 16, v46
	v_cndmask_b32_e64 v106, -v28, v28, s[10:11]
	v_add_co_u32_e32 v28, vcc, s90, v16
	s_movk_i32 s4, 0xc400
	s_nop 0
	v_addc_co_u32_e32 v29, vcc, 0, v17, vcc
	v_sub_u32_e32 v42, 0x400, v18
	v_cmp_eq_u32_e32 vcc, s4, v18
	s_movk_i32 s4, 0xc800
	v_cmp_eq_u32_e64 s[4:5], s4, v18
	v_cndmask_b32_e64 v46, v42, 0, vcc
	v_sub_u32_e32 v42, 0x800, v18
	v_ashrrev_i32_e32 v47, 31, v46
	v_cndmask_b32_e64 v64, v42, 0, s[4:5]
	v_lshl_add_u64 v[46:47], v[46:47], 1, s[2:3]
	v_ashrrev_i32_e32 v65, 31, v64
	v_lshl_add_u64 v[64:65], v[64:65], 1, s[2:3]
	global_load_ushort v42, v[46:47], off
	s_nop 0
	global_load_ushort v46, v[64:65], off
	global_load_ushort v110, v[28:29], off
	global_load_ushort v112, v[28:29], off offset:1024
	global_load_ushort v114, v[28:29], off offset:2048
	global_load_ushort v116, v[28:29], off offset:3072
	s_mov_b32 s10, 0x3f74fa0b
	s_mov_b32 s11, 0xbe94a031
	s_mov_b32 s80, s11
	s_mov_b32 s81, s10
	v_add_f32_e32 v52, v15, v13
	s_mov_b32 s12, 0x3e94a031
	s_mov_b32 s13, 0xbf74fa0b
	s_mov_b32 s64, s13
	s_mov_b32 s65, s12
	s_mov_b32 s8, 0x3e47c5c2
	s_mov_b32 s9, 0xbf7b14be
	s_mov_b32 s30, s9
	s_mov_b32 s31, s8
	s_mov_b32 s6, 0x3f7b14be
	s_mov_b32 s7, 0xbe47c5c2
	s_mov_b32 s6, s9
	s_waitcnt vmcnt(6)
	v_lshlrev_b32_e32 v28, 16, v38
	v_cndmask_b32_e64 v108, -v28, v28, s[0:1]
	s_movk_i32 s0, 0xc600
	v_sub_u32_e32 v28, 0x600, v18
	v_sub_u32_e32 v38, 0x200, v18
	s_waitcnt vmcnt(4)
	v_lshlrev_b32_e32 v29, 16, v46
	v_cndmask_b32_e64 v111, -v29, v29, s[4:5]
	v_cmp_eq_u32_e64 s[4:5], s0, v18
	s_movk_i32 s0, 0xc200
	v_cmp_eq_u32_e64 s[0:1], s0, v18
	v_cndmask_b32_e64 v28, v28, 0, s[4:5]
	v_ashrrev_i32_e32 v29, 31, v28
	v_cndmask_b32_e64 v46, v38, 0, s[0:1]
	v_lshl_add_u64 v[28:29], v[28:29], 1, s[2:3]
	v_ashrrev_i32_e32 v47, 31, v46
	v_lshl_add_u64 v[46:47], v[46:47], 1, s[2:3]
	global_load_ushort v18, v[16:17], off
	s_nop 0
	global_load_ushort v28, v[28:29], off
	s_nop 0
	global_load_ushort v29, v[16:17], off offset:1024
	s_nop 0
	global_load_ushort v17, v[16:17], off offset:2048
	s_nop 0
	global_load_ushort v38, v[46:47], off
	global_load_ushort v56, v[20:21], off offset:1024
	global_load_ushort v58, v[20:21], off offset:2048
	global_load_ushort v60, v[20:21], off offset:3072
	global_load_ushort v62, v[24:25], off offset:-4096
	global_load_ushort v98, v[24:25], off
	global_load_ushort v48, v[20:21], off offset:-4096
	global_load_ushort v64, v[22:23], off offset:1024
	global_load_ushort v68, v[22:23], off offset:2048
	s_nop 0
	global_load_ushort v21, v[20:21], off
	v_lshlrev_b32_e32 v22, 16, v42
	v_cndmask_b32_e64 v115, -v22, v22, vcc
	v_pk_mul_f32 v[22:23], v[14:15], s[78:79] op_sel_hi:[0,1] neg_lo:[1,0]
	s_mov_b64 vcc, s[66:67]
	s_mov_b32 s66, s71
	s_mov_b32 s67, s70
	s_mov_b32 s2, 0x3f7ec46d
	s_mov_b32 s3, 0xbdc8bd36
	s_waitcnt vmcnt(13)
	v_lshlrev_b32_e32 v16, 16, v18
	s_waitcnt vmcnt(12)
	v_lshlrev_b32_e32 v18, 16, v28
	s_waitcnt vmcnt(11)
	v_lshlrev_b32_e32 v20, 16, v29
	s_waitcnt vmcnt(10)
	v_lshlrev_b32_e32 v17, 16, v17
	v_add_f32_e32 v20, v31, v20
	v_pk_fma_f32 v[28:29], v[10:11], s[68:69], v[22:23] op_sel_hi:[0,1,1]
	v_add_f32_e32 v22, v30, v17
	v_pk_mul_f32 v[30:31], v[14:15], s[66:67] op_sel_hi:[0,1] neg_lo:[1,0]
	v_pk_fma_f32 v[46:47], v[10:11], s[70:71], v[30:31] op_sel_hi:[0,1,1]
	v_pk_mul_f32 v[30:31], v[14:15], s[80:81] op_sel_hi:[0,1] neg_lo:[1,0]
	v_pk_fma_f32 v[88:89], v[10:11], s[10:11], v[30:31] op_sel_hi:[0,1,1]
	s_waitcnt vmcnt(3)
	v_lshlrev_b32_e32 v13, 16, v48
	v_pk_mul_f32 v[30:31], v[14:15], s[52:53] op_sel_hi:[0,1] neg_lo:[1,0]
	v_add_f32_e32 v16, v19, v16
	v_cndmask_b32_e64 v113, -v18, v18, s[4:5]
	v_pk_mul_f32 v[18:19], v[14:15], s[40:41] op_sel_hi:[0,1] neg_lo:[1,0]
	v_add_f32_e32 v54, v32, v13
	v_pk_fma_f32 v[66:67], v[10:11], s[94:95], v[30:31] op_sel_hi:[0,1,1]
	s_waitcnt vmcnt(2)
	v_lshlrev_b32_e32 v13, 16, v64
	v_pk_mul_f32 v[30:31], v[14:15], s[50:51] op_sel_hi:[0,1] neg_lo:[1,0]
	s_waitcnt vmcnt(1)
	v_lshlrev_b32_e32 v15, 16, v68
	v_lshlrev_b32_e32 v17, 16, v38
	v_add_f32_e32 v32, v36, v13
	global_load_ushort v13, v[24:25], off offset:1024
	v_add_f32_e32 v38, v37, v15
	global_load_ushort v15, v[24:25], off offset:2048
	v_lshlrev_b32_e32 v23, 16, v33
	s_waitcnt vmcnt(2)
	v_lshlrev_b32_e32 v21, 16, v21
	v_add_f32_e32 v42, v35, v23
	global_load_ushort v23, v[24:25], off offset:3072
	global_load_ushort v33, v[26:27], off
	v_add_f32_e32 v48, v34, v21
	v_lshlrev_b32_e32 v21, 16, v56
	v_add_f32_e32 v56, v45, v21
	global_load_ushort v21, v[26:27], off offset:-4096
	s_mov_b32 s68, s83
	s_mov_b32 s69, s82
	s_mov_b32 s70, s23
	s_mov_b32 s71, s22
	v_pk_fma_f32 v[64:65], v[10:11], s[20:21], v[30:31] op_sel_hi:[0,1,1]
	s_mov_b32 s94, s75
	s_mov_b32 s95, s74
	s_mov_b32 s4, 0x3dc8bd36
	s_mov_b32 s5, 0xbf7ec46d
	s_mov_b32 s34, s5
	s_mov_b32 s35, s4
	s_mov_b32 s2, s5
	v_cndmask_b32_e64 v17, -v17, v17, s[0:1]
	s_mov_b32 s0, s3
	s_mov_b32 s1, s5
	s_mov_b32 s10, s13
	s_mov_b32 s20, s23
	v_pk_fma_f32 v[18:19], v[10:11], s[46:47], v[18:19] op_sel_hi:[0,1,1]
	s_waitcnt vmcnt(4)
	v_lshlrev_b32_e32 v13, 16, v13
	s_waitcnt vmcnt(3)
	v_pk_mul_f32 v[24:25], v[14:15], s[56:57] op_sel_hi:[0,1] neg_lo:[1,0]
	v_pk_fma_f32 v[76:77], v[10:11], s[38:39], v[24:25] op_sel_hi:[0,1,1]
	v_pk_mul_f32 v[24:25], v[14:15], s[62:63] op_sel_hi:[0,1] neg_lo:[1,0]
	v_pk_fma_f32 v[82:83], v[10:11], s[28:29], v[24:25] op_sel_hi:[0,1,1]
	v_lshlrev_b32_e32 v24, 16, v58
	v_add_f32_e32 v58, v44, v24
	v_pk_mul_f32 v[24:25], v[14:15], s[68:69] op_sel_hi:[0,1] neg_lo:[1,0]
	v_pk_fma_f32 v[84:85], v[10:11], s[82:83], v[24:25] op_sel_hi:[0,1,1]
	v_lshlrev_b32_e32 v24, 16, v60
	v_add_f32_e32 v60, v43, v24
	v_pk_mul_f32 v[24:25], v[14:15], s[70:71] op_sel_hi:[0,1] neg_lo:[1,0]
	v_pk_fma_f32 v[86:87], v[10:11], s[22:23], v[24:25] op_sel_hi:[0,1,1]
	v_lshlrev_b32_e32 v24, 16, v62
	v_add_f32_e32 v62, v49, v24
	v_pk_mul_f32 v[24:25], v[14:15], s[58:59] op_sel_hi:[0,1] neg_lo:[1,0]
	v_pk_fma_f32 v[80:81], v[10:11], s[18:19], v[24:25] op_sel_hi:[0,1,1]
	v_lshlrev_b32_e32 v24, 16, v41
	v_add_f32_e32 v50, v50, v24
	v_pk_mul_f32 v[24:25], v[14:15], s[64:65] op_sel_hi:[0,1] neg_lo:[1,0]
	v_pk_fma_f32 v[78:79], v[10:11], s[12:13], v[24:25] op_sel_hi:[0,1,1]
	v_lshlrev_b32_e32 v25, 16, v39
	v_add_f32_e32 v44, v63, v25
	global_load_ushort v25, v[26:27], off offset:1024
	global_load_ushort v39, v[26:27], off offset:2048
	v_lshlrev_b32_e32 v24, 16, v40
	global_load_ushort v40, v[26:27], off offset:3072
	v_pk_mul_f32 v[30:31], v[14:15], s[60:61] op_sel_hi:[0,1] neg_lo:[1,0]
	v_pk_fma_f32 v[68:69], v[10:11], s[24:25], v[30:31] op_sel_hi:[0,1,1]
	v_pk_mul_f32 v[30:31], v[14:15], s[94:95] op_sel_hi:[0,1] neg_lo:[1,0]
	v_pk_fma_f32 v[74:75], v[10:11], s[74:75], v[30:31] op_sel_hi:[0,1,1]
	v_pk_mul_f32 v[30:31], v[14:15], s[30:31] op_sel_hi:[0,1] neg_lo:[1,0]
	v_pk_fma_f32 v[70:71], v[10:11], s[8:9], v[30:31] op_sel_hi:[0,1,1]
	v_pk_mul_f32 v[30:31], v[14:15], s[34:35] op_sel_hi:[0,1] neg_lo:[1,0]
	v_pk_fma_f32 v[72:73], v[10:11], s[4:5], v[30:31] op_sel_hi:[0,1,1]
	v_lshlrev_b32_e32 v30, 16, v98
	v_pk_mul_f32 v[34:35], v[14:15], s[36:37] op_sel_hi:[0,1] neg_lo:[1,0]
	v_add_f32_e32 v30, v90, v30
	v_pk_fma_f32 v[34:35], v[10:11], s[76:77], v[34:35] op_sel_hi:[0,1,1]
	v_pk_mul_f32 v[36:37], v[34:35], v[30:31] op_sel_hi:[1,0]
	v_pk_mul_f32 v[30:31], v[14:15], s[2:3] op_sel_hi:[0,1] neg_lo:[1,0]
	v_add_f32_e32 v26, v59, v13
	v_pk_fma_f32 v[30:31], v[10:11], s[0:1], v[30:31] op_sel_hi:[0,1,1]
	v_lshlrev_b32_e32 v13, 16, v15
	s_mov_b32 s4, s7
	s_mov_b32 s5, s9
	v_pk_mul_f32 v[34:35], v[14:15], s[6:7] op_sel_hi:[0,1] neg_lo:[1,0]
	v_pk_mul_f32 v[26:27], v[30:31], v[26:27] op_sel_hi:[1,0]
	v_add_f32_e32 v30, v57, v13
	v_pk_fma_f32 v[34:35], v[10:11], s[4:5], v[34:35] op_sel_hi:[0,1,1]
	v_pk_mul_f32 v[98:99], v[34:35], v[30:31] op_sel_hi:[1,0]
	s_waitcnt vmcnt(5)
	v_lshlrev_b32_e32 v13, 16, v23
	s_mov_b32 s8, s11
	s_mov_b32 s9, s13
	v_pk_mul_f32 v[34:35], v[14:15], s[10:11] op_sel_hi:[0,1] neg_lo:[1,0]
	v_add_f32_e32 v30, v55, v13
	v_pk_fma_f32 v[34:35], v[10:11], s[8:9], v[34:35] op_sel_hi:[0,1,1]
	v_pk_mul_f32 v[100:101], v[34:35], v[30:31] op_sel_hi:[1,0]
	s_waitcnt vmcnt(3)
	v_lshlrev_b32_e32 v13, 16, v21
	s_mov_b32 s12, s17
	s_mov_b32 s13, s19
	v_pk_mul_f32 v[34:35], v[14:15], s[16:17] op_sel_hi:[0,1] neg_lo:[1,0]
	v_add_f32_e32 v30, v97, v13
	v_pk_fma_f32 v[34:35], v[10:11], s[12:13], v[34:35] op_sel_hi:[0,1,1]
	v_pk_mul_f32 v[102:103], v[34:35], v[30:31] op_sel_hi:[1,0]
	v_lshlrev_b32_e32 v13, 16, v53
	s_mov_b32 s18, s21
	s_mov_b32 s19, s23
	v_pk_mul_f32 v[34:35], v[14:15], s[20:21] op_sel_hi:[0,1] neg_lo:[1,0]
	v_add_f32_e32 v30, v96, v13
	v_pk_fma_f32 v[34:35], v[10:11], s[18:19], v[34:35] op_sel_hi:[0,1,1]
	s_mov_b32 s24, s83
	v_pk_mul_f32 v[96:97], v[34:35], v[30:31] op_sel_hi:[1,0]
	v_lshlrev_b32_e32 v13, 16, v51
	s_mov_b32 s22, s25
	s_mov_b32 s23, s83
	v_pk_mul_f32 v[34:35], v[14:15], s[24:25] op_sel_hi:[0,1] neg_lo:[1,0]
	v_add_f32_e32 v30, v94, v13
	v_pk_fma_f32 v[34:35], v[10:11], s[22:23], v[34:35] op_sel_hi:[0,1,1]
	s_mov_b32 s28, s29
	s_mov_b32 s29, s75
	v_pk_mul_f32 v[104:105], v[34:35], v[30:31] op_sel_hi:[1,0]
	v_lshlrev_b32_e32 v13, 16, v91
	v_pk_mul_f32 v[34:35], v[14:15], s[28:29] op_sel_hi:[0,1] neg_lo:[1,0]
	v_add_f32_e32 v30, v93, v13
	v_pk_fma_f32 v[34:35], v[10:11], s[26:27], v[34:35] op_sel_hi:[0,1,1]
	v_pk_mul_f32 v[90:91], v[34:35], v[30:31] op_sel_hi:[1,0]
	v_lshlrev_b32_e32 v13, 16, v33
	v_pk_mul_f32 v[34:35], v[14:15], s[38:39] op_sel_hi:[0,0] neg_lo:[1,0]
	s_mov_b32 s38, s39
	v_add_f32_e32 v30, v92, v13
	v_pk_fma_f32 v[34:35], v[10:11], s[38:39], v[34:35] op_sel_hi:[0,0,1] neg_lo:[0,0,1] neg_hi:[0,0,1]
	v_pk_mul_f32 v[92:93], v[34:35], v[30:31] op_sel_hi:[1,0]
	v_pk_mul_f32 v[34:35], v[14:15], s[26:27] op_sel_hi:[0,1] neg_lo:[1,0]
	v_pk_fma_f32 v[34:35], v[10:11], s[28:29], v[34:35] op_sel_hi:[0,1,1]
	v_add_f32_e32 v24, v61, v24
	s_waitcnt vmcnt(2)
	v_lshlrev_b32_e32 v13, 16, v25
	v_add_f32_e32 v30, v95, v13
	v_pk_mul_f32 v[94:95], v[34:35], v[30:31] op_sel_hi:[1,0]
	s_waitcnt vmcnt(1)
	v_lshlrev_b32_e32 v13, 16, v39
	v_pk_mul_f32 v[34:35], v[14:15], s[22:23] op_sel_hi:[0,1] neg_lo:[1,0]
	v_add_f32_e32 v30, v106, v13
	v_pk_fma_f32 v[34:35], v[10:11], s[24:25], v[34:35] op_sel_hi:[0,1,1]
	v_pk_mul_f32 v[106:107], v[34:35], v[30:31] op_sel_hi:[1,0]
	s_waitcnt vmcnt(0)
	v_lshlrev_b32_e32 v13, 16, v40
	v_pk_mul_f32 v[34:35], v[14:15], s[18:19] op_sel_hi:[0,1] neg_lo:[1,0]
	v_add_f32_e32 v30, v108, v13
	v_pk_fma_f32 v[34:35], v[10:11], s[20:21], v[34:35] op_sel_hi:[0,1,1]
	v_pk_mul_f32 v[108:109], v[34:35], v[30:31] op_sel_hi:[1,0]
	v_lshlrev_b32_e32 v13, 16, v110
	v_pk_mul_f32 v[34:35], v[14:15], s[12:13] op_sel_hi:[0,1] neg_lo:[1,0]
	v_add_f32_e32 v30, v111, v13
	v_pk_fma_f32 v[34:35], v[10:11], s[16:17], v[34:35] op_sel_hi:[0,1,1]
	v_pk_mul_f32 v[110:111], v[34:35], v[30:31] op_sel_hi:[1,0]
	v_lshlrev_b32_e32 v13, 16, v112
	v_pk_mul_f32 v[34:35], v[14:15], s[8:9] op_sel_hi:[0,1] neg_lo:[1,0]
	v_add_f32_e32 v30, v113, v13
	v_pk_fma_f32 v[34:35], v[10:11], s[10:11], v[34:35] op_sel_hi:[0,1,1]
	v_pk_mul_f32 v[112:113], v[34:35], v[30:31] op_sel_hi:[1,0]
	v_lshlrev_b32_e32 v13, 16, v114
	v_pk_mul_f32 v[34:35], v[14:15], s[4:5] op_sel_hi:[0,1] neg_lo:[1,0]
	v_add_f32_e32 v30, v115, v13
	v_pk_fma_f32 v[34:35], v[10:11], s[6:7], v[34:35] op_sel_hi:[0,1,1]
	v_lshlrev_b32_e32 v13, 16, v116
	v_pk_mul_f32 v[14:15], v[14:15], s[0:1] op_sel_hi:[0,1] neg_lo:[1,0]
	v_pk_mul_f32 v[114:115], v[34:35], v[30:31] op_sel_hi:[1,0]
	v_add_f32_e32 v30, v17, v13
	v_pk_fma_f32 v[14:15], v[10:11], s[2:3], v[14:15] op_sel_hi:[0,1,1]
	v_pk_mul_f32 v[116:117], v[14:15], v[30:31] op_sel_hi:[1,0]
	v_mov_b32_e32 v13, v174
	v_mov_b32_e32 v30, v166
	v_mov_b32_e32 v10, v168
	v_mov_b32_e32 v34, v170
	v_mov_b32_e32 v17, v172
	s_nop 0
	v_pk_fma_f32 v[126:127], v[18:19], v[16:17], v[36:37] op_sel_hi:[1,0,1]
	v_pk_fma_f32 v[36:37], v[18:19], v[16:17], v[36:37] op_sel_hi:[1,0,1] neg_lo:[0,0,1] neg_hi:[0,0,1]
	v_pk_fma_f32 v[18:19], v[28:29], v[20:21], v[26:27] op_sel_hi:[1,0,1] neg_lo:[0,0,1] neg_hi:[0,0,1]
	v_pk_fma_f32 v[16:17], v[28:29], v[20:21], v[26:27] op_sel_hi:[1,0,1]
	v_pk_mul_f32 v[20:21], v[18:19], v[124:125] op_sel:[1,0] op_sel_hi:[0,0] neg_lo:[1,1] neg_hi:[0,1]
	s_nop 0
	v_pk_fma_f32 v[40:41], v[18:19], v[118:119], v[20:21] op_sel_hi:[1,0,1]
	v_pk_fma_f32 v[20:21], v[46:47], v[22:23], v[98:99] op_sel_hi:[1,0,1] neg_lo:[0,0,1] neg_hi:[0,0,1]
	v_pk_fma_f32 v[18:19], v[46:47], v[22:23], v[98:99] op_sel_hi:[1,0,1]
	v_pk_mul_f32 v[22:23], v[20:21], v[34:35] op_sel:[1,0] op_sel_hi:[0,0] neg_lo:[1,1] neg_hi:[0,1]
	s_nop 0
	v_pk_fma_f32 v[46:47], v[20:21], v[30:31], v[22:23] op_sel_hi:[1,0,1]
	v_pk_fma_f32 v[22:23], v[88:89], v[52:53], v[100:101] op_sel_hi:[1,0,1] neg_lo:[0,0,1] neg_hi:[0,0,1]
	v_pk_fma_f32 v[20:21], v[88:89], v[52:53], v[100:101] op_sel_hi:[1,0,1]
	v_pk_mul_f32 v[26:27], v[22:23], v[122:123] op_sel:[1,0] op_sel_hi:[0,0] neg_lo:[1,1] neg_hi:[0,1]
	s_nop 0
	v_pk_fma_f32 v[52:53], v[22:23], v[120:121], v[26:27] op_sel_hi:[1,0,1]
	v_pk_fma_f32 v[26:27], v[66:67], v[54:55], v[102:103] op_sel_hi:[1,0,1] neg_lo:[0,0,1] neg_hi:[0,0,1]
	v_pk_fma_f32 v[22:23], v[66:67], v[54:55], v[102:103] op_sel_hi:[1,0,1]
	v_pk_mul_f32 v[28:29], v[26:27], v[10:11] op_sel:[1,0] op_sel_hi:[0,0] neg_lo:[1,1] neg_hi:[0,1]
	s_nop 0
	v_pk_fma_f32 v[54:55], v[26:27], v[10:11], v[28:29] op_sel_hi:[1,0,1]
	v_pk_fma_f32 v[28:29], v[64:65], v[32:33], v[96:97] op_sel_hi:[1,0,1] neg_lo:[0,0,1] neg_hi:[0,0,1]
	v_pk_fma_f32 v[26:27], v[64:65], v[32:33], v[96:97] op_sel_hi:[1,0,1]
	v_pk_mul_f32 v[32:33], v[28:29], v[122:123] op_sel_hi:[1,0]
	s_nop 0
	v_pk_fma_f32 v[64:65], v[28:29], v[120:121], v[32:33] op_sel:[1,0,0] op_sel_hi:[0,0,1] neg_lo:[1,1,0] neg_hi:[0,1,0]
	v_pk_fma_f32 v[32:33], v[68:69], v[38:39], v[104:105] op_sel_hi:[1,0,1] neg_lo:[0,0,1] neg_hi:[0,0,1]
	v_pk_fma_f32 v[28:29], v[68:69], v[38:39], v[104:105] op_sel_hi:[1,0,1]
	v_pk_mul_f32 v[38:39], v[32:33], v[34:35] op_sel_hi:[1,0]
	s_nop 0
	v_pk_fma_f32 v[66:67], v[32:33], v[30:31], v[38:39] op_sel:[1,0,0] op_sel_hi:[0,0,1] neg_lo:[1,1,0] neg_hi:[0,1,0]
	v_pk_fma_f32 v[38:39], v[74:75], v[42:43], v[90:91] op_sel_hi:[1,0,1] neg_lo:[0,0,1] neg_hi:[0,0,1]
	v_pk_fma_f32 v[32:33], v[74:75], v[42:43], v[90:91] op_sel_hi:[1,0,1]
	v_pk_mul_f32 v[42:43], v[38:39], v[124:125] op_sel_hi:[1,0]
	s_nop 0
	v_pk_fma_f32 v[68:69], v[38:39], v[118:119], v[42:43] op_sel:[1,0,0] op_sel_hi:[0,0,1] neg_lo:[1,1,0] neg_hi:[0,1,0]
	v_pk_fma_f32 v[38:39], v[76:77], v[48:49], v[92:93] op_sel_hi:[1,0,1]
	v_pk_fma_f32 v[42:43], v[76:77], v[48:49], v[92:93] op_sel_hi:[1,0,1] neg_lo:[0,0,1] neg_hi:[0,0,1]
	v_pk_fma_f32 v[48:49], v[82:83], v[56:57], v[94:95] op_sel_hi:[1,0,1] neg_lo:[0,0,1] neg_hi:[0,0,1]
	v_xor_b32_e32 v75, 0x80000000, v42
	v_mov_b32_e32 v74, v43
	v_pk_fma_f32 v[42:43], v[82:83], v[56:57], v[94:95] op_sel_hi:[1,0,1]
	v_pk_mul_f32 v[56:57], v[48:49], v[124:125] op_sel_hi:[1,0] neg_lo:[0,1] neg_hi:[0,1]
	v_xor_b32_e32 v76, 0x80000000, v49
	v_mov_b32_e32 v77, v48
	v_pk_fma_f32 v[48:49], v[84:85], v[58:59], v[106:107] op_sel_hi:[1,0,1]
	v_pk_fma_f32 v[58:59], v[84:85], v[58:59], v[106:107] op_sel_hi:[1,0,1] neg_lo:[0,0,1] neg_hi:[0,0,1]
	v_pk_fma_f32 v[56:57], v[76:77], v[118:119], v[56:57] op_sel_hi:[1,0,1] neg_lo:[0,1,0] neg_hi:[0,1,0]
	v_pk_mul_f32 v[76:77], v[58:59], v[34:35] op_sel_hi:[1,0] neg_lo:[0,1] neg_hi:[0,1]
	s_nop 0
	v_pk_fma_f32 v[58:59], v[58:59], v[30:31], v[76:77] op_sel:[1,0,0] op_sel_hi:[0,0,1] neg_lo:[1,1,0] neg_hi:[0,1,0]
	v_pk_fma_f32 v[76:77], v[86:87], v[60:61], v[108:109] op_sel_hi:[1,0,1]
	v_pk_fma_f32 v[60:61], v[86:87], v[60:61], v[108:109] op_sel_hi:[1,0,1] neg_lo:[0,0,1] neg_hi:[0,0,1]
	s_nop 0
	v_pk_mul_f32 v[82:83], v[60:61], v[122:123] op_sel_hi:[1,0] neg_lo:[0,1] neg_hi:[0,1]
	s_nop 0
	v_pk_fma_f32 v[60:61], v[60:61], v[120:121], v[82:83] op_sel:[1,0,0] op_sel_hi:[0,0,1] neg_lo:[1,1,0] neg_hi:[0,1,0]
	v_pk_fma_f32 v[82:83], v[80:81], v[62:63], v[110:111] op_sel_hi:[1,0,1]
	v_pk_fma_f32 v[62:63], v[80:81], v[62:63], v[110:111] op_sel_hi:[1,0,1] neg_lo:[0,0,1] neg_hi:[0,0,1]
	v_pk_add_f32 v[84:85], v[126:127], v[38:39] neg_lo:[0,1] neg_hi:[0,1]
	v_pk_mul_f32 v[80:81], v[62:63], v[10:11] op_sel:[1,0] op_sel_hi:[0,0] neg_lo:[1,1] neg_hi:[0,1]
	s_nop 0
	v_pk_fma_f32 v[62:63], v[62:63], v[10:11], v[80:81] op_sel_hi:[1,0,1] neg_lo:[0,1,0] neg_hi:[0,1,0]
	v_pk_fma_f32 v[80:81], v[78:79], v[50:51], v[112:113] op_sel_hi:[1,0,1]
	v_pk_fma_f32 v[50:51], v[78:79], v[50:51], v[112:113] op_sel_hi:[1,0,1] neg_lo:[0,0,1] neg_hi:[0,0,1]
	s_nop 0
	v_pk_mul_f32 v[78:79], v[50:51], v[122:123] op_sel:[1,0] op_sel_hi:[0,0] neg_lo:[1,1] neg_hi:[0,1]
	s_nop 0
	v_pk_fma_f32 v[50:51], v[50:51], v[120:121], v[78:79] op_sel_hi:[1,0,1] neg_lo:[0,1,0] neg_hi:[0,1,0]
	v_pk_fma_f32 v[78:79], v[70:71], v[24:25], v[114:115] op_sel_hi:[1,0,1]
	v_pk_fma_f32 v[24:25], v[70:71], v[24:25], v[114:115] op_sel_hi:[1,0,1] neg_lo:[0,0,1] neg_hi:[0,0,1]
	s_nop 0
	v_pk_mul_f32 v[70:71], v[24:25], v[34:35] op_sel:[1,0] op_sel_hi:[0,0] neg_lo:[1,1] neg_hi:[0,1]
	s_nop 0
	v_pk_fma_f32 v[70:71], v[24:25], v[30:31], v[70:71] op_sel_hi:[1,0,1] neg_lo:[0,1,0] neg_hi:[0,1,0]
	v_pk_fma_f32 v[24:25], v[72:73], v[44:45], v[116:117] op_sel_hi:[1,0,1]
	v_pk_fma_f32 v[44:45], v[72:73], v[44:45], v[116:117] op_sel_hi:[1,0,1] neg_lo:[0,0,1] neg_hi:[0,0,1]
	s_nop 0
	v_pk_mul_f32 v[72:73], v[44:45], v[124:125] op_sel:[1,0] op_sel_hi:[0,0] neg_lo:[1,1] neg_hi:[0,1]
	s_nop 0
	v_pk_fma_f32 v[72:73], v[118:119], v[44:45], v[72:73] op_sel_hi:[0,1,1] neg_lo:[1,0,0] neg_hi:[1,0,0]
	v_pk_add_f32 v[44:45], v[126:127], v[38:39]
	v_pk_add_f32 v[38:39], v[16:17], v[42:43]
	v_pk_add_f32 v[16:17], v[16:17], v[42:43] neg_lo:[0,1] neg_hi:[0,1]
	s_nop 0
	v_pk_mul_f32 v[42:43], v[16:17], v[34:35] op_sel:[1,0] op_sel_hi:[0,0] neg_lo:[1,1] neg_hi:[0,1]
	s_nop 0
	v_pk_fma_f32 v[42:43], v[16:17], v[30:31], v[42:43] op_sel_hi:[1,0,1]
	v_pk_add_f32 v[16:17], v[18:19], v[48:49]
	v_pk_add_f32 v[18:19], v[18:19], v[48:49] neg_lo:[0,1] neg_hi:[0,1]
	s_nop 0
	v_pk_mul_f32 v[48:49], v[18:19], v[10:11] op_sel:[1,0] op_sel_hi:[0,0] neg_lo:[1,1] neg_hi:[0,1]
	s_nop 0
	v_pk_fma_f32 v[18:19], v[18:19], v[10:11], v[48:49] op_sel_hi:[1,0,1]
	v_pk_add_f32 v[48:49], v[20:21], v[76:77]
	v_pk_add_f32 v[20:21], v[20:21], v[76:77] neg_lo:[0,1] neg_hi:[0,1]
	s_nop 0
	v_pk_mul_f32 v[76:77], v[20:21], v[34:35] op_sel_hi:[1,0]
	v_xor_b32_e32 v86, 0x80000000, v21
	v_mov_b32_e32 v87, v20
	v_pk_add_f32 v[20:21], v[22:23], v[82:83]
	v_pk_add_f32 v[22:23], v[22:23], v[82:83] neg_lo:[0,1] neg_hi:[0,1]
	v_pk_fma_f32 v[76:77], v[86:87], v[30:31], v[76:77] op_sel_hi:[1,0,1] neg_lo:[0,1,0] neg_hi:[0,1,0]
	v_xor_b32_e32 v83, 0x80000000, v22
	v_mov_b32_e32 v82, v23
	v_pk_add_f32 v[22:23], v[26:27], v[80:81]
	v_pk_add_f32 v[26:27], v[26:27], v[80:81] neg_lo:[0,1] neg_hi:[0,1]
	s_nop 0
	v_pk_mul_f32 v[80:81], v[26:27], v[34:35] op_sel_hi:[1,0] neg_lo:[0,1] neg_hi:[0,1]
	s_nop 0
	v_pk_fma_f32 v[26:27], v[30:31], v[26:27], v[80:81] op_sel:[0,1,0] op_sel_hi:[0,0,1] neg_lo:[1,1,0] neg_hi:[1,0,0]
	v_pk_add_f32 v[80:81], v[28:29], v[78:79]
	v_pk_add_f32 v[28:29], v[28:29], v[78:79] neg_lo:[0,1] neg_hi:[0,1]
	v_pk_add_f32 v[86:87], v[44:45], v[20:21] neg_lo:[0,1] neg_hi:[0,1]
	v_pk_mul_f32 v[78:79], v[10:11], v[28:29] op_sel:[0,1] op_sel_hi:[0,0] neg_lo:[1,1] neg_hi:[1,0]
	v_pk_fma_f32 v[78:79], v[28:29], v[10:11], v[78:79] op_sel_hi:[1,0,1] neg_lo:[0,1,0] neg_hi:[0,1,0]
	v_pk_add_f32 v[28:29], v[32:33], v[24:25]
	v_pk_add_f32 v[24:25], v[32:33], v[24:25] neg_lo:[0,1] neg_hi:[0,1]
	s_nop 0
	v_pk_mul_f32 v[32:33], v[34:35], v[24:25] op_sel:[0,1] op_sel_hi:[0,0] neg_lo:[1,1] neg_hi:[1,0]
	v_pk_fma_f32 v[32:33], v[30:31], v[24:25], v[32:33] op_sel_hi:[0,1,1] neg_lo:[1,0,0] neg_hi:[1,0,0]
	v_pk_add_f32 v[24:25], v[44:45], v[20:21]
	v_pk_add_f32 v[20:21], v[38:39], v[22:23]
	v_pk_add_f32 v[22:23], v[38:39], v[22:23] neg_lo:[0,1] neg_hi:[0,1]
	s_nop 0
	v_pk_mul_f32 v[38:39], v[10:11], v[22:23] op_sel:[0,1] op_sel_hi:[0,0] neg_lo:[1,1] neg_hi:[1,0]
	v_pk_fma_f32 v[22:23], v[22:23], v[10:11], v[38:39] op_sel_hi:[1,0,1]
	v_pk_add_f32 v[38:39], v[16:17], v[80:81]
	v_pk_add_f32 v[16:17], v[16:17], v[80:81] neg_lo:[0,1] neg_hi:[0,1]
	s_nop 0
	v_xor_b32_e32 v81, 0x80000000, v16
	v_mov_b32_e32 v80, v17
	v_pk_add_f32 v[16:17], v[48:49], v[28:29]
	v_pk_add_f32 v[28:29], v[48:49], v[28:29] neg_lo:[0,1] neg_hi:[0,1]
	s_nop 0
	v_pk_mul_f32 v[44:45], v[10:11], v[28:29] op_sel:[0,1] op_sel_hi:[0,0] neg_lo:[1,1] neg_hi:[1,0]
	v_pk_fma_f32 v[48:49], v[10:11], v[28:29], v[44:45] op_sel_hi:[0,1,1] neg_lo:[1,0,0] neg_hi:[1,0,0]
	v_pk_add_f32 v[28:29], v[24:25], v[38:39]
	v_pk_add_f32 v[24:25], v[24:25], v[38:39] neg_lo:[0,1] neg_hi:[0,1]
	v_pk_add_f32 v[38:39], v[20:21], v[16:17]
	v_pk_add_f32 v[16:17], v[20:21], v[16:17] neg_lo:[0,1] neg_hi:[0,1]
	v_pk_add_f32 v[88:89], v[28:29], v[38:39]
	v_pk_add_f32 v[44:45], v[24:25], v[16:17] op_sel:[0,1] op_sel_hi:[1,0] neg_hi:[0,1]
	v_pk_add_f32 v[20:21], v[24:25], v[16:17] op_sel:[0,1] op_sel_hi:[1,0] neg_lo:[0,1]
	v_pk_add_f32 v[24:25], v[22:23], v[48:49]
	v_pk_add_f32 v[22:23], v[22:23], v[48:49] neg_lo:[0,1] neg_hi:[0,1]
	v_pk_add_f32 v[16:17], v[86:87], v[80:81]
	v_pk_add_f32 v[80:81], v[86:87], v[80:81] neg_lo:[0,1] neg_hi:[0,1]
	v_pk_add_f32 v[28:29], v[28:29], v[38:39] neg_lo:[0,1] neg_hi:[0,1]
	v_pk_add_f32 v[86:87], v[16:17], v[24:25]
	v_pk_add_f32 v[24:25], v[16:17], v[24:25] neg_lo:[0,1] neg_hi:[0,1]
	v_pk_add_f32 v[38:39], v[80:81], v[22:23] op_sel:[0,1] op_sel_hi:[1,0] neg_hi:[0,1]
	v_pk_add_f32 v[16:17], v[80:81], v[22:23] op_sel:[0,1] op_sel_hi:[1,0] neg_lo:[0,1]
	v_pk_add_f32 v[48:49], v[42:43], v[26:27]
	v_pk_add_f32 v[26:27], v[42:43], v[26:27] neg_lo:[0,1] neg_hi:[0,1]
	v_pk_add_f32 v[22:23], v[84:85], v[82:83]
	v_pk_mul_f32 v[42:43], v[10:11], v[26:27] op_sel:[0,1] op_sel_hi:[0,0] neg_lo:[1,1] neg_hi:[1,0]
	v_pk_fma_f32 v[26:27], v[10:11], v[26:27], v[42:43] op_sel_hi:[0,1,1]
	v_pk_add_f32 v[42:43], v[18:19], v[78:79]
	v_pk_add_f32 v[18:19], v[18:19], v[78:79] neg_lo:[0,1] neg_hi:[0,1]
	v_pk_add_f32 v[80:81], v[84:85], v[82:83] neg_lo:[0,1] neg_hi:[0,1]
	v_xor_b32_e32 v79, 0x80000000, v18
	v_mov_b32_e32 v78, v19
	v_pk_add_f32 v[18:19], v[76:77], v[32:33]
	v_pk_add_f32 v[32:33], v[76:77], v[32:33] neg_lo:[0,1] neg_hi:[0,1]
	s_nop 0
	v_pk_mul_f32 v[76:77], v[10:11], v[32:33] op_sel:[0,1] op_sel_hi:[0,0] neg_lo:[1,1] neg_hi:[1,0]
	v_pk_fma_f32 v[76:77], v[10:11], v[32:33], v[76:77] op_sel_hi:[0,1,1] neg_lo:[1,0,0] neg_hi:[1,0,0]
	v_pk_add_f32 v[32:33], v[22:23], v[42:43]
	v_pk_add_f32 v[22:23], v[22:23], v[42:43] neg_lo:[0,1] neg_hi:[0,1]
	v_pk_add_f32 v[42:43], v[48:49], v[18:19]
	v_pk_add_f32 v[18:19], v[48:49], v[18:19] neg_lo:[0,1] neg_hi:[0,1]
	v_pk_add_f32 v[84:85], v[32:33], v[42:43]
	v_pk_add_f32 v[32:33], v[32:33], v[42:43] neg_lo:[0,1] neg_hi:[0,1]
	v_pk_add_f32 v[42:43], v[26:27], v[76:77]
	v_pk_add_f32 v[26:27], v[26:27], v[76:77] neg_lo:[0,1] neg_hi:[0,1]
	v_xor_b32_e32 v83, 0x80000000, v18
	v_mov_b32_e32 v82, v19
	v_pk_add_f32 v[18:19], v[80:81], v[78:79]
	v_pk_add_f32 v[78:79], v[80:81], v[78:79] neg_lo:[0,1] neg_hi:[0,1]
	v_xor_b32_e32 v77, 0x80000000, v26
	v_mov_b32_e32 v76, v27
	v_pk_add_f32 v[80:81], v[18:19], v[42:43]
	v_pk_add_f32 v[26:27], v[18:19], v[42:43] neg_lo:[0,1] neg_hi:[0,1]
	v_pk_add_f32 v[42:43], v[78:79], v[76:77]
	v_pk_add_f32 v[18:19], v[78:79], v[76:77] neg_lo:[0,1] neg_hi:[0,1]
	v_pk_add_f32 v[76:77], v[36:37], v[74:75]
	v_pk_add_f32 v[74:75], v[36:37], v[74:75] neg_lo:[0,1] neg_hi:[0,1]
	v_pk_add_f32 v[36:37], v[40:41], v[56:57]
	v_pk_add_f32 v[40:41], v[40:41], v[56:57] neg_lo:[0,1] neg_hi:[0,1]
	v_pk_add_f32 v[48:49], v[22:23], v[82:83]
	v_pk_mul_f32 v[56:57], v[34:35], v[40:41] op_sel:[0,1] op_sel_hi:[0,0] neg_lo:[1,1] neg_hi:[1,0]
	v_pk_fma_f32 v[40:41], v[30:31], v[40:41], v[56:57] op_sel_hi:[0,1,1]
	v_pk_add_f32 v[56:57], v[46:47], v[58:59]
	v_pk_add_f32 v[46:47], v[46:47], v[58:59] neg_lo:[0,1] neg_hi:[0,1]
	v_pk_add_f32 v[22:23], v[22:23], v[82:83] neg_lo:[0,1] neg_hi:[0,1]
	v_pk_mul_f32 v[58:59], v[10:11], v[46:47] op_sel:[0,1] op_sel_hi:[0,0] neg_lo:[1,1] neg_hi:[1,0]
	v_pk_fma_f32 v[58:59], v[10:11], v[46:47], v[58:59] op_sel_hi:[0,1,1]
	v_pk_add_f32 v[46:47], v[52:53], v[60:61]
	v_pk_add_f32 v[52:53], v[52:53], v[60:61] neg_lo:[0,1] neg_hi:[0,1]
	s_nop 0
	v_pk_mul_f32 v[60:61], v[30:31], v[52:53] op_sel:[0,1] op_sel_hi:[0,0] neg_lo:[1,1] neg_hi:[1,0]
	v_pk_fma_f32 v[60:61], v[34:35], v[52:53], v[60:61] op_sel_hi:[0,1,1]
	v_pk_add_f32 v[52:53], v[54:55], v[62:63]
	v_pk_add_f32 v[54:55], v[54:55], v[62:63] neg_lo:[0,1] neg_hi:[0,1]
	s_nop 0
	v_xor_b32_e32 v63, 0x80000000, v54
	v_mov_b32_e32 v62, v55
	v_pk_add_f32 v[54:55], v[64:65], v[50:51]
	v_pk_add_f32 v[50:51], v[64:65], v[50:51] neg_lo:[0,1] neg_hi:[0,1]
	s_nop 0
	v_pk_mul_f32 v[64:65], v[30:31], v[50:51] op_sel:[0,1] op_sel_hi:[0,0] neg_lo:[1,1] neg_hi:[1,0]
	v_pk_fma_f32 v[50:51], v[34:35], v[50:51], v[64:65] op_sel_hi:[0,1,1] neg_lo:[1,0,0] neg_hi:[1,0,0]
	v_pk_add_f32 v[64:65], v[66:67], v[70:71]
	v_pk_add_f32 v[66:67], v[66:67], v[70:71] neg_lo:[0,1] neg_hi:[0,1]
	s_nop 0
	v_pk_mul_f32 v[70:71], v[10:11], v[66:67] op_sel:[0,1] op_sel_hi:[0,0] neg_lo:[1,1] neg_hi:[1,0]
	v_pk_fma_f32 v[66:67], v[10:11], v[66:67], v[70:71] op_sel_hi:[0,1,1] neg_lo:[1,0,0] neg_hi:[1,0,0]
	v_pk_add_f32 v[70:71], v[68:69], v[72:73]
	v_pk_add_f32 v[68:69], v[68:69], v[72:73] neg_lo:[0,1] neg_hi:[0,1]
	s_nop 0
	v_pk_mul_f32 v[34:35], v[34:35], v[68:69] op_sel:[0,1] op_sel_hi:[0,0] neg_lo:[1,1] neg_hi:[1,0]
	v_pk_fma_f32 v[34:35], v[30:31], v[68:69], v[34:35] op_sel_hi:[0,1,1] neg_lo:[1,0,0] neg_hi:[1,0,0]
	v_pk_add_f32 v[30:31], v[76:77], v[52:53]
	v_pk_add_f32 v[68:69], v[76:77], v[52:53] neg_lo:[0,1] neg_hi:[0,1]
	v_pk_add_f32 v[52:53], v[54:55], v[36:37]
	v_pk_add_f32 v[36:37], v[36:37], v[54:55] neg_lo:[0,1] neg_hi:[0,1]
	s_nop 0
	v_pk_mul_f32 v[54:55], v[10:11], v[36:37] op_sel:[0,1] op_sel_hi:[0,0] neg_lo:[1,1] neg_hi:[1,0]
	v_pk_fma_f32 v[54:55], v[10:11], v[36:37], v[54:55] op_sel_hi:[0,1,1]
	v_pk_add_f32 v[36:37], v[56:57], v[64:65]
	v_pk_add_f32 v[56:57], v[56:57], v[64:65] neg_lo:[0,1] neg_hi:[0,1]
	s_nop 0
	v_xor_b32_e32 v65, 0x80000000, v56
	v_mov_b32_e32 v64, v57
	v_pk_add_f32 v[56:57], v[46:47], v[70:71]
	v_pk_add_f32 v[46:47], v[46:47], v[70:71] neg_lo:[0,1] neg_hi:[0,1]
	s_nop 0
	v_pk_mul_f32 v[70:71], v[10:11], v[46:47] op_sel:[0,1] op_sel_hi:[0,0] neg_lo:[1,1] neg_hi:[1,0]
	v_pk_fma_f32 v[46:47], v[10:11], v[46:47], v[70:71] op_sel_hi:[0,1,1] neg_lo:[1,0,0] neg_hi:[1,0,0]
	v_pk_add_f32 v[70:71], v[30:31], v[36:37]
	v_pk_add_f32 v[30:31], v[30:31], v[36:37] neg_lo:[0,1] neg_hi:[0,1]
	v_pk_add_f32 v[36:37], v[52:53], v[56:57]
	v_pk_add_f32 v[52:53], v[52:53], v[56:57] neg_lo:[0,1] neg_hi:[0,1]
	v_pk_add_f32 v[72:73], v[70:71], v[36:37]
	v_xor_b32_e32 v57, 0x80000000, v52
	v_mov_b32_e32 v56, v53
	v_pk_add_f32 v[52:53], v[70:71], v[36:37] neg_lo:[0,1] neg_hi:[0,1]
	v_pk_add_f32 v[70:71], v[30:31], v[56:57]
	v_pk_add_f32 v[36:37], v[30:31], v[56:57] neg_lo:[0,1] neg_hi:[0,1]
	v_pk_add_f32 v[30:31], v[68:69], v[64:65]
	v_pk_add_f32 v[56:57], v[68:69], v[64:65] neg_lo:[0,1] neg_hi:[0,1]
	v_pk_add_f32 v[64:65], v[54:55], v[46:47]
	v_pk_add_f32 v[46:47], v[54:55], v[46:47] neg_lo:[0,1] neg_hi:[0,1]
	v_pk_add_f32 v[68:69], v[30:31], v[64:65]
	v_xor_b32_e32 v55, 0x80000000, v46
	v_mov_b32_e32 v54, v47
	v_pk_add_f32 v[46:47], v[30:31], v[64:65] neg_lo:[0,1] neg_hi:[0,1]
	v_pk_add_f32 v[64:65], v[56:57], v[54:55]
	v_pk_add_f32 v[30:31], v[56:57], v[54:55] neg_lo:[0,1] neg_hi:[0,1]
	v_pk_add_f32 v[54:55], v[74:75], v[62:63]
	v_pk_add_f32 v[56:57], v[74:75], v[62:63] neg_lo:[0,1] neg_hi:[0,1]
	v_pk_add_f32 v[62:63], v[50:51], v[40:41]
	v_pk_add_f32 v[40:41], v[40:41], v[50:51] neg_lo:[0,1] neg_hi:[0,1]
	s_nop 0
	v_pk_mul_f32 v[50:51], v[10:11], v[40:41] op_sel:[0,1] op_sel_hi:[0,0] neg_lo:[1,1] neg_hi:[1,0]
	v_pk_fma_f32 v[50:51], v[10:11], v[40:41], v[50:51] op_sel_hi:[0,1,1]
	v_pk_add_f32 v[40:41], v[58:59], v[66:67]
	v_pk_add_f32 v[58:59], v[58:59], v[66:67] neg_lo:[0,1] neg_hi:[0,1]
	s_nop 0
	v_xor_b32_e32 v67, 0x80000000, v58
	v_mov_b32_e32 v66, v59
	v_pk_add_f32 v[58:59], v[60:61], v[34:35]
	v_pk_add_f32 v[34:35], v[60:61], v[34:35] neg_lo:[0,1] neg_hi:[0,1]
	s_nop 0
	v_pk_mul_f32 v[60:61], v[10:11], v[34:35] op_sel:[0,1] op_sel_hi:[0,0] neg_lo:[1,1] neg_hi:[1,0]
	v_pk_fma_f32 v[34:35], v[10:11], v[34:35], v[60:61] op_sel_hi:[0,1,1] neg_lo:[1,0,0] neg_hi:[1,0,0]
	v_pk_add_f32 v[60:61], v[54:55], v[40:41]
	v_pk_add_f32 v[40:41], v[54:55], v[40:41] neg_lo:[0,1] neg_hi:[0,1]
	v_pk_add_f32 v[54:55], v[62:63], v[58:59]
	v_pk_add_f32 v[58:59], v[62:63], v[58:59] neg_lo:[0,1] neg_hi:[0,1]
	v_lshl_add_u32 v10, v13, 3, 0
	v_xor_b32_e32 v63, 0x80000000, v58
	v_mov_b32_e32 v62, v59
	v_pk_add_f32 v[58:59], v[60:61], v[54:55]
	v_pk_add_f32 v[54:55], v[60:61], v[54:55] neg_lo:[0,1] neg_hi:[0,1]
	v_pk_add_f32 v[60:61], v[40:41], v[62:63]
	v_pk_add_f32 v[40:41], v[40:41], v[62:63] neg_lo:[0,1] neg_hi:[0,1]
	v_pk_add_f32 v[62:63], v[56:57], v[66:67]
	v_pk_add_f32 v[56:57], v[56:57], v[66:67] neg_lo:[0,1] neg_hi:[0,1]
	v_pk_add_f32 v[66:67], v[50:51], v[34:35]
	v_pk_add_f32 v[34:35], v[50:51], v[34:35] neg_lo:[0,1] neg_hi:[0,1]
	v_pk_add_f32 v[76:77], v[62:63], v[66:67]
	v_pk_add_f32 v[50:51], v[62:63], v[66:67] neg_lo:[0,1] neg_hi:[0,1]
	v_pk_add_f32 v[62:63], v[56:57], v[34:35] op_sel:[0,1] op_sel_hi:[1,0] neg_hi:[0,1]
	v_pk_add_f32 v[34:35], v[56:57], v[34:35] op_sel:[0,1] op_sel_hi:[1,0] neg_lo:[0,1]
	v_pk_mul_f32 v[56:57], v[88:89], s[14:15] op_sel:[1,0] neg_lo:[1,0]
	s_nop 0
	v_pk_fma_f32 v[56:57], v[88:89], s[42:43], v[56:57] op_sel_hi:[0,1,1]
	ds_write_b64 v10, v[56:57]
	v_pk_fma_f32 v[56:57], v[180:181], s[92:93], v[180:181] op_sel:[1,0,0] op_sel_hi:[0,1,1]
	v_pk_mul_f32 v[66:67], v[56:57], v[72:73] op_sel:[1,1] op_sel_hi:[0,1] neg_lo:[0,1]
	v_pk_fma_f32 v[66:67], v[56:57], v[72:73], v[66:67] op_sel_hi:[1,0,1]
	ds_write_b64 v10, v[66:67] offset:4224
	v_pk_mul_f32 v[66:67], v[180:181], v[56:57] op_sel:[1,1] op_sel_hi:[0,1] neg_lo:[0,1]
	v_pk_fma_f32 v[56:57], v[180:181], v[56:57], v[66:67] op_sel_hi:[1,0,1]
	s_nop 0
	v_pk_mul_f32 v[66:67], v[56:57], v[84:85] op_sel:[1,1] op_sel_hi:[0,1] neg_lo:[0,1]
	v_pk_fma_f32 v[66:67], v[56:57], v[84:85], v[66:67] op_sel_hi:[1,0,1]
	ds_write_b64 v10, v[66:67] offset:8448
	v_pk_mul_f32 v[66:67], v[180:181], v[56:57] op_sel:[1,1] op_sel_hi:[0,1] neg_lo:[0,1]
	v_pk_fma_f32 v[56:57], v[180:181], v[56:57], v[66:67] op_sel_hi:[1,0,1]
	s_nop 0
	v_pk_mul_f32 v[66:67], v[56:57], v[58:59] op_sel:[1,1] op_sel_hi:[0,1] neg_lo:[0,1]
	v_pk_fma_f32 v[58:59], v[56:57], v[58:59], v[66:67] op_sel_hi:[1,0,1]
	ds_write_b64 v10, v[58:59] offset:12672
	v_pk_mul_f32 v[58:59], v[180:181], v[56:57] op_sel:[1,1] op_sel_hi:[0,1] neg_lo:[0,1]
	v_pk_fma_f32 v[56:57], v[180:181], v[56:57], v[58:59] op_sel_hi:[1,0,1]
	s_nop 0
	v_pk_mul_f32 v[58:59], v[56:57], v[86:87] op_sel:[1,1] op_sel_hi:[0,1] neg_lo:[0,1]
	v_pk_fma_f32 v[58:59], v[56:57], v[86:87], v[58:59] op_sel_hi:[1,0,1]
	ds_write_b64 v10, v[58:59] offset:16896
	v_pk_mul_f32 v[58:59], v[180:181], v[56:57] op_sel:[1,1] op_sel_hi:[0,1] neg_lo:[0,1]
	v_pk_fma_f32 v[56:57], v[180:181], v[56:57], v[58:59] op_sel_hi:[1,0,1]
	s_nop 0
	v_pk_mul_f32 v[58:59], v[56:57], v[68:69] op_sel:[1,1] op_sel_hi:[0,1] neg_lo:[0,1]
	v_pk_fma_f32 v[58:59], v[56:57], v[68:69], v[58:59] op_sel_hi:[1,0,1]
	ds_write_b64 v10, v[58:59] offset:21120
	v_pk_mul_f32 v[58:59], v[180:181], v[56:57] op_sel:[1,1] op_sel_hi:[0,1] neg_lo:[0,1]
	v_pk_fma_f32 v[56:57], v[180:181], v[56:57], v[58:59] op_sel_hi:[1,0,1]
	s_nop 0
	v_pk_mul_f32 v[58:59], v[80:81], v[56:57] op_sel:[1,1] op_sel_hi:[1,0] neg_lo:[1,0]
	s_nop 0
	v_pk_fma_f32 v[58:59], v[80:81], v[56:57], v[58:59] op_sel_hi:[0,1,1]
	ds_write_b64 v10, v[58:59] offset:25344
	v_pk_mul_f32 v[58:59], v[180:181], v[56:57] op_sel:[1,1] op_sel_hi:[0,1] neg_lo:[0,1]
	v_pk_fma_f32 v[56:57], v[180:181], v[56:57], v[58:59] op_sel_hi:[1,0,1]
	s_nop 0
	v_pk_mul_f32 v[58:59], v[76:77], v[56:57] op_sel:[1,1] op_sel_hi:[1,0] neg_lo:[1,0]
	s_nop 0
	v_pk_fma_f32 v[58:59], v[76:77], v[56:57], v[58:59] op_sel_hi:[0,1,1]
	ds_write_b64 v10, v[58:59] offset:29568
	v_pk_mul_f32 v[58:59], v[180:181], v[56:57] op_sel:[1,1] op_sel_hi:[0,1] neg_lo:[0,1]
	v_pk_fma_f32 v[56:57], v[180:181], v[56:57], v[58:59] op_sel_hi:[1,0,1]
	s_nop 0
	v_pk_mul_f32 v[58:59], v[44:45], v[56:57] op_sel:[1,1] op_sel_hi:[1,0] neg_lo:[1,0]
	s_nop 0
	v_pk_fma_f32 v[44:45], v[44:45], v[56:57], v[58:59] op_sel_hi:[0,1,1]
	ds_write_b64 v10, v[44:45] offset:33792
	v_pk_mul_f32 v[44:45], v[180:181], v[56:57] op_sel:[1,1] op_sel_hi:[0,1] neg_lo:[0,1]
	v_pk_fma_f32 v[44:45], v[180:181], v[56:57], v[44:45] op_sel_hi:[1,0,1]
	s_nop 0
	v_pk_mul_f32 v[56:57], v[70:71], v[44:45] op_sel:[1,1] op_sel_hi:[1,0] neg_lo:[1,0]
	s_nop 0
	v_pk_fma_f32 v[56:57], v[70:71], v[44:45], v[56:57] op_sel_hi:[0,1,1]
	ds_write_b64 v10, v[56:57] offset:38016
	v_pk_mul_f32 v[56:57], v[180:181], v[44:45] op_sel:[1,1] op_sel_hi:[0,1] neg_lo:[0,1]
	v_pk_fma_f32 v[44:45], v[180:181], v[44:45], v[56:57] op_sel_hi:[1,0,1]
	s_nop 0
	v_pk_mul_f32 v[56:57], v[48:49], v[44:45] op_sel:[1,1] op_sel_hi:[1,0] neg_lo:[1,0]
	s_nop 0
	v_pk_fma_f32 v[48:49], v[48:49], v[44:45], v[56:57] op_sel_hi:[0,1,1]
	ds_write_b64 v10, v[48:49] offset:42240
	v_pk_mul_f32 v[48:49], v[180:181], v[44:45] op_sel:[1,1] op_sel_hi:[0,1] neg_lo:[0,1]
	v_pk_fma_f32 v[44:45], v[180:181], v[44:45], v[48:49] op_sel_hi:[1,0,1]
	s_nop 0
	v_pk_mul_f32 v[48:49], v[60:61], v[44:45] op_sel:[1,1] op_sel_hi:[1,0] neg_lo:[1,0]
	s_nop 0
	v_pk_fma_f32 v[48:49], v[60:61], v[44:45], v[48:49] op_sel_hi:[0,1,1]
	ds_write_b64 v10, v[48:49] offset:46464
	v_pk_mul_f32 v[48:49], v[180:181], v[44:45] op_sel:[1,1] op_sel_hi:[0,1] neg_lo:[0,1]
	v_pk_fma_f32 v[44:45], v[180:181], v[44:45], v[48:49] op_sel_hi:[1,0,1]
	s_nop 0
	v_pk_mul_f32 v[48:49], v[38:39], v[44:45] op_sel:[1,1] op_sel_hi:[1,0] neg_lo:[1,0]
	s_nop 0
	v_pk_fma_f32 v[38:39], v[38:39], v[44:45], v[48:49] op_sel_hi:[0,1,1]
	ds_write_b64 v10, v[38:39] offset:50688
	v_pk_mul_f32 v[38:39], v[180:181], v[44:45] op_sel:[1,1] op_sel_hi:[0,1] neg_lo:[0,1]
	v_pk_fma_f32 v[38:39], v[180:181], v[44:45], v[38:39] op_sel_hi:[1,0,1]
	s_nop 0
	v_pk_mul_f32 v[44:45], v[64:65], v[38:39] op_sel:[1,1] op_sel_hi:[1,0] neg_lo:[1,0]
	s_nop 0
	v_pk_fma_f32 v[44:45], v[64:65], v[38:39], v[44:45] op_sel_hi:[0,1,1]
	ds_write_b64 v10, v[44:45] offset:54912
	v_pk_mul_f32 v[44:45], v[180:181], v[38:39] op_sel:[1,1] op_sel_hi:[0,1] neg_lo:[0,1]
	v_pk_fma_f32 v[38:39], v[180:181], v[38:39], v[44:45] op_sel_hi:[1,0,1]
	s_nop 0
	v_pk_mul_f32 v[44:45], v[42:43], v[38:39] op_sel:[1,1] op_sel_hi:[1,0] neg_lo:[1,0]
	s_nop 0
	v_pk_fma_f32 v[42:43], v[42:43], v[38:39], v[44:45] op_sel_hi:[0,1,1]
	ds_write_b64 v10, v[42:43] offset:59136
	v_pk_mul_f32 v[42:43], v[180:181], v[38:39] op_sel:[1,1] op_sel_hi:[0,1] neg_lo:[0,1]
	v_pk_fma_f32 v[38:39], v[180:181], v[38:39], v[42:43] op_sel_hi:[1,0,1]
	s_nop 0
	v_pk_mul_f32 v[42:43], v[62:63], v[38:39] op_sel:[1,1] op_sel_hi:[1,0] neg_lo:[1,0]
	s_nop 0
	v_pk_fma_f32 v[42:43], v[62:63], v[38:39], v[42:43] op_sel_hi:[0,1,1]
	ds_write_b64 v10, v[42:43] offset:63360
	v_pk_mul_f32 v[42:43], v[180:181], v[38:39] op_sel:[1,1] op_sel_hi:[0,1] neg_lo:[0,1]
	v_pk_fma_f32 v[38:39], v[180:181], v[38:39], v[42:43] op_sel_hi:[1,0,1]
	s_nop 0
	v_pk_mul_f32 v[42:43], v[28:29], v[38:39] op_sel:[1,1] op_sel_hi:[1,0] neg_lo:[1,0]
	v_add_u32_e32 v13, 0x10800, v10
	v_pk_fma_f32 v[28:29], v[28:29], v[38:39], v[42:43] op_sel_hi:[0,1,1]
	ds_write_b64 v13, v[28:29]
	v_pk_mul_f32 v[28:29], v[180:181], v[38:39] op_sel:[1,1] op_sel_hi:[0,1] neg_lo:[0,1]
	v_pk_fma_f32 v[28:29], v[180:181], v[38:39], v[28:29] op_sel_hi:[1,0,1]
	s_nop 0
	v_pk_mul_f32 v[38:39], v[52:53], v[28:29] op_sel:[1,1] op_sel_hi:[1,0] neg_lo:[1,0]
	v_add_u32_e32 v13, 0x11880, v10
	v_pk_fma_f32 v[38:39], v[52:53], v[28:29], v[38:39] op_sel_hi:[0,1,1]
	ds_write_b64 v13, v[38:39]
	v_pk_mul_f32 v[38:39], v[180:181], v[28:29] op_sel:[1,1] op_sel_hi:[0,1] neg_lo:[0,1]
	v_pk_fma_f32 v[28:29], v[180:181], v[28:29], v[38:39] op_sel_hi:[1,0,1]
	s_nop 0
	v_pk_mul_f32 v[38:39], v[32:33], v[28:29] op_sel:[1,1] op_sel_hi:[1,0] neg_lo:[1,0]
	v_add_u32_e32 v13, 0x12900, v10
	v_pk_fma_f32 v[32:33], v[32:33], v[28:29], v[38:39] op_sel_hi:[0,1,1]
	ds_write_b64 v13, v[32:33]
	v_pk_mul_f32 v[32:33], v[180:181], v[28:29] op_sel:[1,1] op_sel_hi:[0,1] neg_lo:[0,1]
	v_pk_fma_f32 v[28:29], v[180:181], v[28:29], v[32:33] op_sel_hi:[1,0,1]
	s_nop 0
	v_pk_mul_f32 v[32:33], v[54:55], v[28:29] op_sel:[1,1] op_sel_hi:[1,0] neg_lo:[1,0]
	v_add_u32_e32 v13, 0x13980, v10
	v_pk_fma_f32 v[32:33], v[54:55], v[28:29], v[32:33] op_sel_hi:[0,1,1]
	ds_write_b64 v13, v[32:33]
	v_pk_mul_f32 v[32:33], v[180:181], v[28:29] op_sel:[1,1] op_sel_hi:[0,1] neg_lo:[0,1]
	v_pk_fma_f32 v[28:29], v[180:181], v[28:29], v[32:33] op_sel_hi:[1,0,1]
	s_nop 0
	v_pk_mul_f32 v[32:33], v[24:25], v[28:29] op_sel:[1,1] op_sel_hi:[1,0] neg_lo:[1,0]
	v_add_u32_e32 v13, 0x14a00, v10
	v_pk_fma_f32 v[24:25], v[24:25], v[28:29], v[32:33] op_sel_hi:[0,1,1]
	ds_write_b64 v13, v[24:25]
	v_pk_mul_f32 v[24:25], v[180:181], v[28:29] op_sel:[1,1] op_sel_hi:[0,1] neg_lo:[0,1]
	v_pk_fma_f32 v[24:25], v[180:181], v[28:29], v[24:25] op_sel_hi:[1,0,1]
	s_nop 0
	v_pk_mul_f32 v[28:29], v[46:47], v[24:25] op_sel:[1,1] op_sel_hi:[1,0] neg_lo:[1,0]
	v_add_u32_e32 v13, 0x15a80, v10
	v_pk_fma_f32 v[28:29], v[46:47], v[24:25], v[28:29] op_sel_hi:[0,1,1]
	ds_write_b64 v13, v[28:29]
	v_pk_mul_f32 v[28:29], v[180:181], v[24:25] op_sel:[1,1] op_sel_hi:[0,1] neg_lo:[0,1]
	v_pk_fma_f32 v[24:25], v[180:181], v[24:25], v[28:29] op_sel_hi:[1,0,1]
	s_nop 0
	v_pk_mul_f32 v[28:29], v[26:27], v[24:25] op_sel:[1,1] op_sel_hi:[1,0] neg_lo:[1,0]
	v_add_u32_e32 v13, 0x16b00, v10
	v_pk_fma_f32 v[26:27], v[26:27], v[24:25], v[28:29] op_sel_hi:[0,1,1]
	ds_write_b64 v13, v[26:27]
	v_pk_mul_f32 v[26:27], v[180:181], v[24:25] op_sel:[1,1] op_sel_hi:[0,1] neg_lo:[0,1]
	v_pk_fma_f32 v[24:25], v[180:181], v[24:25], v[26:27] op_sel_hi:[1,0,1]
	s_nop 0
	v_pk_mul_f32 v[26:27], v[50:51], v[24:25] op_sel:[1,1] op_sel_hi:[1,0] neg_lo:[1,0]
	v_add_u32_e32 v13, 0x17b80, v10
	v_pk_fma_f32 v[26:27], v[50:51], v[24:25], v[26:27] op_sel_hi:[0,1,1]
	ds_write_b64 v13, v[26:27]
	v_pk_mul_f32 v[26:27], v[180:181], v[24:25] op_sel:[1,1] op_sel_hi:[0,1] neg_lo:[0,1]
	v_pk_fma_f32 v[24:25], v[180:181], v[24:25], v[26:27] op_sel_hi:[1,0,1]
	s_nop 0
	v_pk_mul_f32 v[26:27], v[20:21], v[24:25] op_sel:[1,1] op_sel_hi:[1,0] neg_lo:[1,0]
	v_add_u32_e32 v13, 0x18c00, v10
	v_pk_fma_f32 v[20:21], v[20:21], v[24:25], v[26:27] op_sel_hi:[0,1,1]
	ds_write_b64 v13, v[20:21]
	v_pk_mul_f32 v[20:21], v[180:181], v[24:25] op_sel:[1,1] op_sel_hi:[0,1] neg_lo:[0,1]
	v_pk_fma_f32 v[20:21], v[180:181], v[24:25], v[20:21] op_sel_hi:[1,0,1]
	s_nop 0
	v_pk_mul_f32 v[24:25], v[36:37], v[20:21] op_sel:[1,1] op_sel_hi:[1,0] neg_lo:[1,0]
	v_add_u32_e32 v13, 0x19c80, v10
	v_pk_fma_f32 v[24:25], v[36:37], v[20:21], v[24:25] op_sel_hi:[0,1,1]
	ds_write_b64 v13, v[24:25]
	v_pk_mul_f32 v[24:25], v[180:181], v[20:21] op_sel:[1,1] op_sel_hi:[0,1] neg_lo:[0,1]
	v_pk_fma_f32 v[20:21], v[180:181], v[20:21], v[24:25] op_sel_hi:[1,0,1]
	s_nop 0
	v_pk_mul_f32 v[24:25], v[22:23], v[20:21] op_sel:[1,1] op_sel_hi:[1,0] neg_lo:[1,0]
	v_add_u32_e32 v13, 0x1ad00, v10
	v_pk_fma_f32 v[22:23], v[22:23], v[20:21], v[24:25] op_sel_hi:[0,1,1]
	ds_write_b64 v13, v[22:23]
	v_pk_mul_f32 v[22:23], v[180:181], v[20:21] op_sel:[1,1] op_sel_hi:[0,1] neg_lo:[0,1]
	v_pk_fma_f32 v[20:21], v[180:181], v[20:21], v[22:23] op_sel_hi:[1,0,1]
	s_nop 0
	v_pk_mul_f32 v[22:23], v[40:41], v[20:21] op_sel:[1,1] op_sel_hi:[1,0] neg_lo:[1,0]
	v_add_u32_e32 v13, 0x1bd80, v10
	v_pk_fma_f32 v[22:23], v[40:41], v[20:21], v[22:23] op_sel_hi:[0,1,1]
	ds_write_b64 v13, v[22:23]
	v_pk_mul_f32 v[22:23], v[180:181], v[20:21] op_sel:[1,1] op_sel_hi:[0,1] neg_lo:[0,1]
	v_pk_fma_f32 v[20:21], v[180:181], v[20:21], v[22:23] op_sel_hi:[1,0,1]
	s_nop 0
	v_pk_mul_f32 v[22:23], v[16:17], v[20:21] op_sel:[1,1] op_sel_hi:[1,0] neg_lo:[1,0]
	v_add_u32_e32 v13, 0x1ce00, v10
	v_pk_fma_f32 v[16:17], v[16:17], v[20:21], v[22:23] op_sel_hi:[0,1,1]
	ds_write_b64 v13, v[16:17]
	v_pk_mul_f32 v[16:17], v[180:181], v[20:21] op_sel:[1,1] op_sel_hi:[0,1] neg_lo:[0,1]
	v_pk_fma_f32 v[16:17], v[180:181], v[20:21], v[16:17] op_sel_hi:[1,0,1]
	s_nop 0
	v_pk_mul_f32 v[20:21], v[30:31], v[16:17] op_sel:[1,1] op_sel_hi:[1,0] neg_lo:[1,0]
	v_add_u32_e32 v13, 0x1de80, v10
	v_pk_fma_f32 v[20:21], v[30:31], v[16:17], v[20:21] op_sel_hi:[0,1,1]
	ds_write_b64 v13, v[20:21]
	v_pk_mul_f32 v[20:21], v[180:181], v[16:17] op_sel:[1,1] op_sel_hi:[0,1] neg_lo:[0,1]
	v_pk_fma_f32 v[16:17], v[180:181], v[16:17], v[20:21] op_sel_hi:[1,0,1]
	s_nop 0
	v_pk_mul_f32 v[20:21], v[18:19], v[16:17] op_sel:[1,1] op_sel_hi:[1,0] neg_lo:[1,0]
	v_add_u32_e32 v13, 0x1ef00, v10
	v_pk_fma_f32 v[18:19], v[18:19], v[16:17], v[20:21] op_sel_hi:[0,1,1]
	ds_write_b64 v13, v[18:19]
	v_pk_mul_f32 v[18:19], v[180:181], v[16:17] op_sel:[1,1] op_sel_hi:[0,1] neg_lo:[0,1]
	v_pk_fma_f32 v[14:15], v[180:181], v[16:17], v[18:19] op_sel_hi:[1,0,1]
	s_nop 0
	v_pk_mul_f32 v[16:17], v[34:35], v[14:15] op_sel:[1,1] op_sel_hi:[1,0] neg_lo:[1,0]
	v_add_u32_e32 v10, 0x1ff80, v10
	v_pk_fma_f32 v[14:15], v[34:35], v[14:15], v[16:17] op_sel_hi:[0,1,1]
	ds_write_b64 v10, v[14:15]
	v_mov_b32_e32 v10, v176
	v_mov_b32_e32 v13, v173
	s_waitcnt lgkmcnt(0)
	s_barrier
	v_mov_b32_e32 v14, v182
	v_xad_u32 v28, v13, 3, v10
	v_lshl_add_u32 v71, v28, 3, 0
	v_xad_u32 v28, v13, 4, v10
	v_lshl_add_u32 v70, v28, 3, 0
	v_xad_u32 v28, v13, 5, v10
	v_lshl_add_u32 v69, v28, 3, 0
	v_xad_u32 v28, v13, 6, v10
	v_lshl_add_u32 v68, v28, 3, 0
	v_xad_u32 v28, v13, 7, v10
	v_lshl_add_u32 v67, v28, 3, 0
	v_xad_u32 v28, v13, 8, v10
	v_lshl_add_u32 v28, v28, 3, 0
	v_add_u32_e32 v66, 0x800, v28
	v_xad_u32 v28, v13, 9, v10
	v_lshl_add_u32 v28, v28, 3, 0
	v_add_u32_e32 v65, 0x800, v28
	v_xad_u32 v28, v13, 10, v10
	v_lshl_add_u32 v28, v28, 3, 0
	v_add_u32_e32 v64, 0x800, v28
	v_xad_u32 v28, v13, 11, v10
	v_lshl_add_u32 v28, v28, 3, 0
	v_add_u32_e32 v16, v13, v10
	v_add_u32_e32 v63, 0x800, v28
	v_xad_u32 v28, v13, 12, v10
	v_mov_b32_e32 v15, v183
	v_lshl_add_u32 v74, v16, 3, 0
	v_lshl_add_u32 v28, v28, 3, 0
	ds_read2_b64 v[16:19], v74 offset1:16
	ds_read2_b64 v[38:41], v66 offset1:16
	v_add_u32_e32 v62, 0x800, v28
	v_xad_u32 v28, v13, 13, v10
	v_xad_u32 v20, v13, 1, v10
	v_lshl_add_u32 v28, v28, 3, 0
	v_lshl_add_u32 v73, v20, 3, 0
	v_xad_u32 v24, v13, 2, v10
	v_add_u32_e32 v61, 0x800, v28
	v_xad_u32 v28, v13, 14, v10
	v_xad_u32 v10, v13, 15, v10
	ds_read2_b64 v[20:23], v73 offset0:32 offset1:48
	ds_read2_b64 v[46:49], v65 offset0:32 offset1:48
	v_lshl_add_u32 v28, v28, 3, 0
	v_lshl_add_u32 v10, v10, 3, 0
	v_lshl_add_u32 v72, v24, 3, 0
	v_add_u32_e32 v60, 0x800, v28
	v_add_u32_e32 v13, 0x800, v10
	ds_read2_b64 v[24:27], v72 offset0:64 offset1:80
	ds_read2_b64 v[56:59], v71 offset0:96 offset1:112
	ds_read2_b64 v[76:79], v70 offset0:128 offset1:144
	ds_read2_b64 v[80:83], v69 offset0:160 offset1:176
	ds_read2_b64 v[84:87], v68 offset0:192 offset1:208
	ds_read2_b64 v[88:91], v67 offset0:224 offset1:240
	ds_read2_b64 v[52:55], v64 offset0:64 offset1:80
	ds_read2_b64 v[92:95], v63 offset0:96 offset1:112
	ds_read2_b64 v[96:99], v62 offset0:128 offset1:144
	ds_read2_b64 v[100:103], v61 offset0:160 offset1:176
	ds_read2_b64 v[104:107], v60 offset0:192 offset1:208
	ds_read2_b64 v[108:111], v13 offset0:224 offset1:240
	s_waitcnt lgkmcnt(14)
	v_pk_add_f32 v[112:113], v[16:17], v[38:39]
	v_pk_add_f32 v[38:39], v[16:17], v[38:39] neg_lo:[0,1] neg_hi:[0,1]
	v_pk_add_f32 v[16:17], v[18:19], v[40:41]
	v_pk_add_f32 v[18:19], v[18:19], v[40:41] neg_lo:[0,1] neg_hi:[0,1]
	v_mov_b32_e32 v28, v165
	v_mov_b32_e32 v30, v166
	v_mov_b32_e32 v32, v167
	v_mov_b32_e32 v10, v168
	v_mov_b32_e32 v36, v169
	v_mov_b32_e32 v34, v170
	v_mov_b32_e32 v44, v171
	v_mov_b32_e32 v29, v172
	v_pk_mul_f32 v[40:41], v[18:19], v[44:45] op_sel:[1,0] op_sel_hi:[0,0] neg_lo:[1,1] neg_hi:[0,1]
	s_nop 0
	v_pk_fma_f32 v[42:43], v[18:19], v[28:29], v[40:41] op_sel_hi:[1,0,1]
	s_waitcnt lgkmcnt(12)
	v_pk_add_f32 v[18:19], v[20:21], v[46:47]
	v_pk_add_f32 v[20:21], v[20:21], v[46:47] neg_lo:[0,1] neg_hi:[0,1]
	s_nop 0
	v_pk_mul_f32 v[40:41], v[20:21], v[34:35] op_sel:[1,0] op_sel_hi:[0,0] neg_lo:[1,1] neg_hi:[0,1]
	s_nop 0
	v_pk_fma_f32 v[46:47], v[20:21], v[30:31], v[40:41] op_sel_hi:[1,0,1]
	v_pk_add_f32 v[20:21], v[22:23], v[48:49]
	v_pk_add_f32 v[22:23], v[22:23], v[48:49] neg_lo:[0,1] neg_hi:[0,1]
	s_nop 0
	v_pk_mul_f32 v[40:41], v[22:23], v[36:37] op_sel:[1,0] op_sel_hi:[0,0] neg_lo:[1,1] neg_hi:[0,1]
	s_nop 0
	v_pk_fma_f32 v[50:51], v[22:23], v[32:33], v[40:41] op_sel_hi:[1,0,1]
	s_waitcnt lgkmcnt(5)
	v_pk_add_f32 v[22:23], v[24:25], v[52:53]
	v_pk_add_f32 v[24:25], v[24:25], v[52:53] neg_lo:[0,1] neg_hi:[0,1]
	s_nop 0
	v_pk_mul_f32 v[40:41], v[24:25], v[10:11] op_sel:[1,0] op_sel_hi:[0,0] neg_lo:[1,1] neg_hi:[0,1]
	s_nop 0
	v_pk_fma_f32 v[52:53], v[24:25], v[10:11], v[40:41] op_sel_hi:[1,0,1]
	v_pk_add_f32 v[24:25], v[26:27], v[54:55]
	v_pk_add_f32 v[26:27], v[26:27], v[54:55] neg_lo:[0,1] neg_hi:[0,1]
	s_nop 0
	v_pk_mul_f32 v[40:41], v[26:27], v[36:37] op_sel_hi:[1,0]
	s_nop 0
	v_pk_fma_f32 v[54:55], v[26:27], v[32:33], v[40:41] op_sel:[1,0,0] op_sel_hi:[0,0,1] neg_lo:[1,1,0] neg_hi:[0,1,0]
	s_waitcnt lgkmcnt(4)
	v_pk_add_f32 v[40:41], v[56:57], v[92:93] neg_lo:[0,1] neg_hi:[0,1]
	v_pk_add_f32 v[26:27], v[56:57], v[92:93]
	v_pk_mul_f32 v[48:49], v[40:41], v[34:35] op_sel_hi:[1,0]
	s_nop 0
	v_pk_fma_f32 v[56:57], v[40:41], v[30:31], v[48:49] op_sel:[1,0,0] op_sel_hi:[0,0,1] neg_lo:[1,1,0] neg_hi:[0,1,0]
	v_pk_add_f32 v[48:49], v[58:59], v[94:95] neg_lo:[0,1] neg_hi:[0,1]
	v_pk_add_f32 v[40:41], v[58:59], v[94:95]
	v_pk_mul_f32 v[58:59], v[48:49], v[44:45] op_sel_hi:[1,0]
	v_xor_b32_e32 v92, 0x80000000, v49
	v_mov_b32_e32 v93, v48
	s_waitcnt lgkmcnt(3)
	v_pk_add_f32 v[48:49], v[76:77], v[96:97]
	v_pk_add_f32 v[76:77], v[76:77], v[96:97] neg_lo:[0,1] neg_hi:[0,1]
	v_pk_fma_f32 v[58:59], v[92:93], v[28:29], v[58:59] op_sel_hi:[1,0,1] neg_lo:[0,1,0] neg_hi:[0,1,0]
	v_xor_b32_e32 v93, 0x80000000, v76
	v_mov_b32_e32 v92, v77
	v_pk_add_f32 v[76:77], v[78:79], v[98:99]
	v_pk_add_f32 v[78:79], v[78:79], v[98:99] neg_lo:[0,1] neg_hi:[0,1]
	s_nop 0
	v_pk_mul_f32 v[94:95], v[78:79], v[44:45] op_sel_hi:[1,0] neg_lo:[0,1] neg_hi:[0,1]
	s_nop 0
	v_pk_fma_f32 v[78:79], v[78:79], v[28:29], v[94:95] op_sel:[1,0,0] op_sel_hi:[0,0,1] neg_lo:[1,1,0] neg_hi:[0,1,0]
	s_waitcnt lgkmcnt(2)
	v_pk_add_f32 v[94:95], v[80:81], v[100:101]
	v_pk_add_f32 v[80:81], v[80:81], v[100:101] neg_lo:[0,1] neg_hi:[0,1]
	s_nop 0
	v_pk_mul_f32 v[96:97], v[80:81], v[34:35] op_sel_hi:[1,0] neg_lo:[0,1] neg_hi:[0,1]
	s_nop 0
	v_pk_fma_f32 v[80:81], v[80:81], v[30:31], v[96:97] op_sel:[1,0,0] op_sel_hi:[0,0,1] neg_lo:[1,1,0] neg_hi:[0,1,0]
	v_pk_add_f32 v[96:97], v[82:83], v[102:103]
	v_pk_add_f32 v[82:83], v[82:83], v[102:103] neg_lo:[0,1] neg_hi:[0,1]
	s_nop 0
	v_pk_mul_f32 v[98:99], v[82:83], v[36:37] op_sel_hi:[1,0] neg_lo:[0,1] neg_hi:[0,1]
	s_nop 0
	v_pk_fma_f32 v[82:83], v[82:83], v[32:33], v[98:99] op_sel:[1,0,0] op_sel_hi:[0,0,1] neg_lo:[1,1,0] neg_hi:[0,1,0]
	s_waitcnt lgkmcnt(1)
	v_pk_add_f32 v[98:99], v[84:85], v[104:105]
	v_pk_add_f32 v[84:85], v[84:85], v[104:105] neg_lo:[0,1] neg_hi:[0,1]
	s_nop 0
	v_pk_mul_f32 v[100:101], v[84:85], v[10:11] op_sel:[1,0] op_sel_hi:[0,0] neg_lo:[1,1] neg_hi:[0,1]
	s_nop 0
	v_pk_fma_f32 v[84:85], v[84:85], v[10:11], v[100:101] op_sel_hi:[1,0,1] neg_lo:[0,1,0] neg_hi:[0,1,0]
	v_pk_add_f32 v[100:101], v[86:87], v[106:107]
	v_pk_add_f32 v[86:87], v[86:87], v[106:107] neg_lo:[0,1] neg_hi:[0,1]
	s_nop 0
	v_pk_mul_f32 v[36:37], v[86:87], v[36:37] op_sel:[1,0] op_sel_hi:[0,0] neg_lo:[1,1] neg_hi:[0,1]
	s_nop 0
	v_pk_fma_f32 v[86:87], v[86:87], v[32:33], v[36:37] op_sel_hi:[1,0,1] neg_lo:[0,1,0] neg_hi:[0,1,0]
	s_waitcnt lgkmcnt(0)
	v_pk_add_f32 v[36:37], v[88:89], v[108:109] neg_lo:[0,1] neg_hi:[0,1]
	v_pk_add_f32 v[32:33], v[88:89], v[108:109]
	v_pk_mul_f32 v[88:89], v[36:37], v[34:35] op_sel:[1,0] op_sel_hi:[0,0] neg_lo:[1,1] neg_hi:[0,1]
	s_nop 0
	v_pk_fma_f32 v[88:89], v[36:37], v[30:31], v[88:89] op_sel_hi:[1,0,1] neg_lo:[0,1,0] neg_hi:[0,1,0]
	v_pk_add_f32 v[36:37], v[90:91], v[110:111]
	v_pk_add_f32 v[90:91], v[90:91], v[110:111] neg_lo:[0,1] neg_hi:[0,1]
	s_nop 0
	v_pk_mul_f32 v[44:45], v[90:91], v[44:45] op_sel:[1,0] op_sel_hi:[0,0] neg_lo:[1,1] neg_hi:[0,1]
	s_nop 0
	v_pk_fma_f32 v[90:91], v[90:91], v[28:29], v[44:45] op_sel_hi:[1,0,1] neg_lo:[0,1,0] neg_hi:[0,1,0]
	v_pk_add_f32 v[44:45], v[16:17], v[76:77]
	v_pk_add_f32 v[16:17], v[16:17], v[76:77] neg_lo:[0,1] neg_hi:[0,1]
	v_pk_add_f32 v[28:29], v[112:113], v[48:49]
	v_pk_mul_f32 v[76:77], v[16:17], v[34:35] op_sel:[1,0] op_sel_hi:[0,0] neg_lo:[1,1] neg_hi:[0,1]
	v_pk_add_f32 v[48:49], v[112:113], v[48:49] neg_lo:[0,1] neg_hi:[0,1]
	v_pk_fma_f32 v[76:77], v[16:17], v[30:31], v[76:77] op_sel_hi:[1,0,1]
	v_pk_add_f32 v[16:17], v[18:19], v[94:95]
	v_pk_add_f32 v[18:19], v[18:19], v[94:95] neg_lo:[0,1] neg_hi:[0,1]
	s_nop 0
	v_pk_mul_f32 v[94:95], v[18:19], v[10:11] op_sel:[1,0] op_sel_hi:[0,0] neg_lo:[1,1] neg_hi:[0,1]
	s_nop 0
	v_pk_fma_f32 v[18:19], v[18:19], v[10:11], v[94:95] op_sel_hi:[1,0,1]
	v_pk_add_f32 v[94:95], v[20:21], v[96:97]
	v_pk_add_f32 v[20:21], v[20:21], v[96:97] neg_lo:[0,1] neg_hi:[0,1]
	s_nop 0
	v_pk_mul_f32 v[96:97], v[20:21], v[34:35] op_sel_hi:[1,0]
	v_xor_b32_e32 v102, 0x80000000, v21
	v_mov_b32_e32 v103, v20
	v_pk_add_f32 v[20:21], v[22:23], v[98:99]
	v_pk_add_f32 v[22:23], v[22:23], v[98:99] neg_lo:[0,1] neg_hi:[0,1]
	v_pk_fma_f32 v[96:97], v[102:103], v[30:31], v[96:97] op_sel_hi:[1,0,1] neg_lo:[0,1,0] neg_hi:[0,1,0]
	v_xor_b32_e32 v99, 0x80000000, v22
	v_mov_b32_e32 v98, v23
	v_pk_add_f32 v[22:23], v[24:25], v[100:101]
	v_pk_add_f32 v[24:25], v[24:25], v[100:101] neg_lo:[0,1] neg_hi:[0,1]
	s_nop 0
	v_pk_mul_f32 v[100:101], v[24:25], v[34:35] op_sel_hi:[1,0] neg_lo:[0,1] neg_hi:[0,1]
	v_xor_b32_e32 v102, 0x80000000, v25
	v_mov_b32_e32 v103, v24
	v_pk_add_f32 v[24:25], v[26:27], v[32:33]
	v_pk_add_f32 v[26:27], v[26:27], v[32:33] neg_lo:[0,1] neg_hi:[0,1]
	v_pk_fma_f32 v[100:101], v[102:103], v[30:31], v[100:101] op_sel_hi:[1,0,1] neg_lo:[0,1,0] neg_hi:[0,1,0]
	v_pk_mul_f32 v[32:33], v[26:27], v[10:11] op_sel:[1,0] op_sel_hi:[0,0] neg_lo:[1,1] neg_hi:[0,1]
	v_pk_add_f32 v[102:103], v[28:29], v[20:21] neg_lo:[0,1] neg_hi:[0,1]
	v_pk_fma_f32 v[26:27], v[26:27], v[10:11], v[32:33] op_sel_hi:[1,0,1] neg_lo:[0,1,0] neg_hi:[0,1,0]
	v_pk_add_f32 v[32:33], v[40:41], v[36:37]
	v_pk_add_f32 v[36:37], v[40:41], v[36:37] neg_lo:[0,1] neg_hi:[0,1]
	s_nop 0
	v_pk_mul_f32 v[40:41], v[36:37], v[34:35] op_sel:[1,0] op_sel_hi:[0,0] neg_lo:[1,1] neg_hi:[0,1]
	s_nop 0
	v_pk_fma_f32 v[40:41], v[36:37], v[30:31], v[40:41] op_sel_hi:[1,0,1] neg_lo:[0,1,0] neg_hi:[0,1,0]
	v_pk_add_f32 v[36:37], v[28:29], v[20:21]
	v_pk_add_f32 v[20:21], v[44:45], v[22:23]
	v_pk_add_f32 v[22:23], v[44:45], v[22:23] neg_lo:[0,1] neg_hi:[0,1]
	s_nop 0
	v_pk_mul_f32 v[28:29], v[22:23], v[10:11] op_sel:[1,0] op_sel_hi:[0,0] neg_lo:[1,1] neg_hi:[0,1]
	s_nop 0
	v_pk_fma_f32 v[22:23], v[22:23], v[10:11], v[28:29] op_sel_hi:[1,0,1]
	v_pk_add_f32 v[28:29], v[16:17], v[24:25]
	v_pk_add_f32 v[16:17], v[16:17], v[24:25] neg_lo:[0,1] neg_hi:[0,1]
	s_nop 0
	v_xor_b32_e32 v25, 0x80000000, v16
	v_mov_b32_e32 v24, v17
	v_pk_add_f32 v[16:17], v[94:95], v[32:33]
	v_pk_add_f32 v[32:33], v[94:95], v[32:33] neg_lo:[0,1] neg_hi:[0,1]
	s_nop 0
	v_pk_mul_f32 v[44:45], v[32:33], v[10:11] op_sel:[1,0] op_sel_hi:[0,0] neg_lo:[1,1] neg_hi:[0,1]
	s_nop 0
	v_pk_fma_f32 v[32:33], v[32:33], v[10:11], v[44:45] op_sel_hi:[1,0,1] neg_lo:[0,1,0] neg_hi:[0,1,0]
	v_pk_add_f32 v[44:45], v[36:37], v[28:29]
	v_pk_add_f32 v[36:37], v[36:37], v[28:29] neg_lo:[0,1] neg_hi:[0,1]
	v_pk_add_f32 v[28:29], v[20:21], v[16:17]
	v_pk_add_f32 v[16:17], v[20:21], v[16:17] neg_lo:[0,1] neg_hi:[0,1]
	v_pk_add_f32 v[94:95], v[44:45], v[28:29]
	v_xor_b32_e32 v21, 0x80000000, v16
	v_mov_b32_e32 v20, v17
	v_pk_add_f32 v[16:17], v[102:103], v[24:25]
	v_pk_add_f32 v[102:103], v[102:103], v[24:25] neg_lo:[0,1] neg_hi:[0,1]
	v_pk_add_f32 v[24:25], v[22:23], v[32:33]
	v_pk_add_f32 v[22:23], v[22:23], v[32:33] neg_lo:[0,1] neg_hi:[0,1]
	v_pk_add_f32 v[28:29], v[44:45], v[28:29] neg_lo:[0,1] neg_hi:[0,1]
	v_xor_b32_e32 v33, 0x80000000, v22
	v_mov_b32_e32 v32, v23
	v_pk_add_f32 v[22:23], v[48:49], v[98:99]
	v_pk_add_f32 v[98:99], v[48:49], v[98:99] neg_lo:[0,1] neg_hi:[0,1]
	v_pk_add_f32 v[48:49], v[76:77], v[100:101] neg_lo:[0,1] neg_hi:[0,1]
	v_pk_add_f32 v[44:45], v[36:37], v[20:21]
	v_pk_add_f32 v[20:21], v[36:37], v[20:21] neg_lo:[0,1] neg_hi:[0,1]
	v_pk_add_f32 v[104:105], v[16:17], v[24:25]
	v_pk_add_f32 v[24:25], v[16:17], v[24:25] neg_lo:[0,1] neg_hi:[0,1]
	v_pk_add_f32 v[36:37], v[102:103], v[32:33]
	v_pk_add_f32 v[16:17], v[102:103], v[32:33] neg_lo:[0,1] neg_hi:[0,1]
	v_pk_add_f32 v[32:33], v[76:77], v[100:101]
	v_pk_mul_f32 v[76:77], v[10:11], v[48:49] op_sel:[0,1] op_sel_hi:[0,0] neg_lo:[1,1] neg_hi:[1,0]
	v_pk_fma_f32 v[76:77], v[10:11], v[48:49], v[76:77] op_sel_hi:[0,1,1]
	v_pk_add_f32 v[48:49], v[18:19], v[26:27]
	v_pk_add_f32 v[18:19], v[18:19], v[26:27] neg_lo:[0,1] neg_hi:[0,1]
	s_nop 0
	v_xor_b32_e32 v27, 0x80000000, v18
	v_mov_b32_e32 v26, v19
	v_pk_add_f32 v[18:19], v[96:97], v[40:41]
	v_pk_add_f32 v[40:41], v[96:97], v[40:41] neg_lo:[0,1] neg_hi:[0,1]
	s_nop 0
	v_pk_mul_f32 v[96:97], v[10:11], v[40:41] op_sel:[0,1] op_sel_hi:[0,0] neg_lo:[1,1] neg_hi:[1,0]
	v_pk_fma_f32 v[40:41], v[10:11], v[40:41], v[96:97] op_sel_hi:[0,1,1] neg_lo:[1,0,0] neg_hi:[1,0,0]
	v_pk_add_f32 v[96:97], v[22:23], v[48:49]
	v_pk_add_f32 v[22:23], v[22:23], v[48:49] neg_lo:[0,1] neg_hi:[0,1]
	v_pk_add_f32 v[48:49], v[32:33], v[18:19]
	v_pk_add_f32 v[18:19], v[32:33], v[18:19] neg_lo:[0,1] neg_hi:[0,1]
	v_pk_add_f32 v[102:103], v[96:97], v[48:49]
	v_xor_b32_e32 v101, 0x80000000, v18
	v_mov_b32_e32 v100, v19
	v_pk_add_f32 v[32:33], v[96:97], v[48:49] neg_lo:[0,1] neg_hi:[0,1]
	v_pk_add_f32 v[18:19], v[98:99], v[26:27]
	v_pk_add_f32 v[96:97], v[98:99], v[26:27] neg_lo:[0,1] neg_hi:[0,1]
	v_pk_add_f32 v[26:27], v[76:77], v[40:41]
	v_pk_add_f32 v[40:41], v[76:77], v[40:41] neg_lo:[0,1] neg_hi:[0,1]
	v_pk_add_f32 v[98:99], v[18:19], v[26:27]
	v_xor_b32_e32 v77, 0x80000000, v40
	v_mov_b32_e32 v76, v41
	v_pk_add_f32 v[26:27], v[18:19], v[26:27] neg_lo:[0,1] neg_hi:[0,1]
	v_pk_add_f32 v[40:41], v[96:97], v[76:77]
	v_pk_add_f32 v[18:19], v[96:97], v[76:77] neg_lo:[0,1] neg_hi:[0,1]
	v_pk_add_f32 v[76:77], v[38:39], v[92:93]
	v_pk_add_f32 v[92:93], v[38:39], v[92:93] neg_lo:[0,1] neg_hi:[0,1]
	v_pk_add_f32 v[38:39], v[42:43], v[78:79]
	v_pk_add_f32 v[42:43], v[42:43], v[78:79] neg_lo:[0,1] neg_hi:[0,1]
	v_pk_add_f32 v[48:49], v[22:23], v[100:101]
	v_pk_mul_f32 v[78:79], v[34:35], v[42:43] op_sel:[0,1] op_sel_hi:[0,0] neg_lo:[1,1] neg_hi:[1,0]
	v_pk_fma_f32 v[42:43], v[30:31], v[42:43], v[78:79] op_sel_hi:[0,1,1]
	v_pk_add_f32 v[78:79], v[46:47], v[80:81]
	v_pk_add_f32 v[46:47], v[46:47], v[80:81] neg_lo:[0,1] neg_hi:[0,1]
	v_pk_add_f32 v[22:23], v[22:23], v[100:101] neg_lo:[0,1] neg_hi:[0,1]
	v_pk_mul_f32 v[80:81], v[10:11], v[46:47] op_sel:[0,1] op_sel_hi:[0,0] neg_lo:[1,1] neg_hi:[1,0]
	v_pk_fma_f32 v[80:81], v[10:11], v[46:47], v[80:81] op_sel_hi:[0,1,1]
	v_pk_add_f32 v[46:47], v[50:51], v[82:83]
	v_pk_add_f32 v[50:51], v[50:51], v[82:83] neg_lo:[0,1] neg_hi:[0,1]
	s_nop 0
	v_pk_mul_f32 v[82:83], v[30:31], v[50:51] op_sel:[0,1] op_sel_hi:[0,0] neg_lo:[1,1] neg_hi:[1,0]
	v_pk_fma_f32 v[50:51], v[34:35], v[50:51], v[82:83] op_sel_hi:[0,1,1]
	v_pk_add_f32 v[82:83], v[52:53], v[84:85]
	v_pk_add_f32 v[52:53], v[52:53], v[84:85] neg_lo:[0,1] neg_hi:[0,1]
	s_nop 0
	v_xor_b32_e32 v85, 0x80000000, v52
	v_mov_b32_e32 v84, v53
	v_pk_add_f32 v[52:53], v[54:55], v[86:87]
	v_pk_add_f32 v[54:55], v[54:55], v[86:87] neg_lo:[0,1] neg_hi:[0,1]
	s_nop 0
	v_pk_mul_f32 v[86:87], v[30:31], v[54:55] op_sel:[0,1] op_sel_hi:[0,0] neg_lo:[1,1] neg_hi:[1,0]
	v_pk_fma_f32 v[54:55], v[34:35], v[54:55], v[86:87] op_sel_hi:[0,1,1] neg_lo:[1,0,0] neg_hi:[1,0,0]
	v_pk_add_f32 v[86:87], v[56:57], v[88:89]
	v_pk_add_f32 v[56:57], v[56:57], v[88:89] neg_lo:[0,1] neg_hi:[0,1]
	s_nop 0
	v_pk_mul_f32 v[88:89], v[10:11], v[56:57] op_sel:[0,1] op_sel_hi:[0,0] neg_lo:[1,1] neg_hi:[1,0]
	v_pk_fma_f32 v[56:57], v[10:11], v[56:57], v[88:89] op_sel_hi:[0,1,1] neg_lo:[1,0,0] neg_hi:[1,0,0]
	v_pk_add_f32 v[88:89], v[58:59], v[90:91]
	v_pk_add_f32 v[58:59], v[58:59], v[90:91] neg_lo:[0,1] neg_hi:[0,1]
	s_nop 0
	v_pk_mul_f32 v[34:35], v[34:35], v[58:59] op_sel:[0,1] op_sel_hi:[0,0] neg_lo:[1,1] neg_hi:[1,0]
	v_pk_fma_f32 v[34:35], v[30:31], v[58:59], v[34:35] op_sel_hi:[0,1,1] neg_lo:[1,0,0] neg_hi:[1,0,0]
	v_pk_add_f32 v[30:31], v[76:77], v[82:83]
	v_pk_add_f32 v[58:59], v[76:77], v[82:83] neg_lo:[0,1] neg_hi:[0,1]
	v_pk_add_f32 v[76:77], v[52:53], v[38:39]
	v_pk_add_f32 v[38:39], v[38:39], v[52:53] neg_lo:[0,1] neg_hi:[0,1]
	s_nop 0
	v_pk_mul_f32 v[52:53], v[10:11], v[38:39] op_sel:[0,1] op_sel_hi:[0,0] neg_lo:[1,1] neg_hi:[1,0]
	v_pk_fma_f32 v[52:53], v[10:11], v[38:39], v[52:53] op_sel_hi:[0,1,1]
	v_pk_add_f32 v[38:39], v[78:79], v[86:87]
	v_pk_add_f32 v[78:79], v[78:79], v[86:87] neg_lo:[0,1] neg_hi:[0,1]
	s_nop 0
	v_xor_b32_e32 v83, 0x80000000, v78
	v_mov_b32_e32 v82, v79
	v_pk_add_f32 v[78:79], v[46:47], v[88:89]
	v_pk_add_f32 v[46:47], v[46:47], v[88:89] neg_lo:[0,1] neg_hi:[0,1]
	v_pk_add_f32 v[88:89], v[76:77], v[78:79]
	v_pk_mul_f32 v[86:87], v[10:11], v[46:47] op_sel:[0,1] op_sel_hi:[0,0] neg_lo:[1,1] neg_hi:[1,0]
	v_pk_fma_f32 v[46:47], v[10:11], v[46:47], v[86:87] op_sel_hi:[0,1,1] neg_lo:[1,0,0] neg_hi:[1,0,0]
	v_pk_add_f32 v[86:87], v[30:31], v[38:39]
	v_pk_add_f32 v[30:31], v[30:31], v[38:39] neg_lo:[0,1] neg_hi:[0,1]
	v_pk_add_f32 v[38:39], v[76:77], v[78:79] neg_lo:[0,1] neg_hi:[0,1]
	v_pk_add_f32 v[78:79], v[86:87], v[88:89] neg_lo:[0,1] neg_hi:[0,1]
	v_pk_add_f32 v[90:91], v[30:31], v[38:39] op_sel:[0,1] op_sel_hi:[1,0] neg_hi:[0,1]
	v_pk_add_f32 v[38:39], v[30:31], v[38:39] op_sel:[0,1] op_sel_hi:[1,0] neg_lo:[0,1]
	v_pk_add_f32 v[76:77], v[52:53], v[46:47]
	v_pk_add_f32 v[46:47], v[52:53], v[46:47] neg_lo:[0,1] neg_hi:[0,1]
	v_pk_add_f32 v[30:31], v[58:59], v[82:83]
	v_pk_add_f32 v[58:59], v[58:59], v[82:83] neg_lo:[0,1] neg_hi:[0,1]
	v_xor_b32_e32 v53, 0x80000000, v46
	v_mov_b32_e32 v52, v47
	v_pk_add_f32 v[82:83], v[30:31], v[76:77]
	v_pk_add_f32 v[46:47], v[30:31], v[76:77] neg_lo:[0,1] neg_hi:[0,1]
	v_pk_add_f32 v[76:77], v[58:59], v[52:53]
	v_pk_add_f32 v[30:31], v[58:59], v[52:53] neg_lo:[0,1] neg_hi:[0,1]
	v_pk_add_f32 v[52:53], v[92:93], v[84:85]
	v_pk_add_f32 v[58:59], v[92:93], v[84:85] neg_lo:[0,1] neg_hi:[0,1]
	v_pk_add_f32 v[84:85], v[54:55], v[42:43]
	v_pk_add_f32 v[42:43], v[42:43], v[54:55] neg_lo:[0,1] neg_hi:[0,1]
	v_pk_add_f32 v[86:87], v[86:87], v[88:89]
	v_pk_mul_f32 v[54:55], v[10:11], v[42:43] op_sel:[0,1] op_sel_hi:[0,0] neg_lo:[1,1] neg_hi:[1,0]
	v_pk_fma_f32 v[54:55], v[10:11], v[42:43], v[54:55] op_sel_hi:[0,1,1]
	v_pk_add_f32 v[42:43], v[80:81], v[56:57]
	v_pk_add_f32 v[56:57], v[80:81], v[56:57] neg_lo:[0,1] neg_hi:[0,1]
	s_nop 0
	v_xor_b32_e32 v81, 0x80000000, v56
	v_mov_b32_e32 v80, v57
	v_pk_add_f32 v[56:57], v[50:51], v[34:35]
	v_pk_add_f32 v[34:35], v[50:51], v[34:35] neg_lo:[0,1] neg_hi:[0,1]
	s_nop 0
	v_pk_mul_f32 v[50:51], v[10:11], v[34:35] op_sel:[0,1] op_sel_hi:[0,0] neg_lo:[1,1] neg_hi:[1,0]
	v_pk_fma_f32 v[34:35], v[10:11], v[34:35], v[50:51] op_sel_hi:[0,1,1] neg_lo:[1,0,0] neg_hi:[1,0,0]
	v_pk_add_f32 v[50:51], v[52:53], v[42:43]
	v_pk_add_f32 v[42:43], v[52:53], v[42:43] neg_lo:[0,1] neg_hi:[0,1]
	v_pk_add_f32 v[52:53], v[84:85], v[56:57]
	v_pk_add_f32 v[56:57], v[84:85], v[56:57] neg_lo:[0,1] neg_hi:[0,1]
	s_nop 0
	v_xor_b32_e32 v85, 0x80000000, v56
	v_mov_b32_e32 v84, v57
	v_pk_add_f32 v[56:57], v[50:51], v[52:53]
	v_pk_add_f32 v[50:51], v[50:51], v[52:53] neg_lo:[0,1] neg_hi:[0,1]
	v_pk_add_f32 v[52:53], v[42:43], v[84:85]
	v_pk_add_f32 v[42:43], v[42:43], v[84:85] neg_lo:[0,1] neg_hi:[0,1]
	v_pk_add_f32 v[84:85], v[58:59], v[80:81]
	v_pk_add_f32 v[58:59], v[58:59], v[80:81] neg_lo:[0,1] neg_hi:[0,1]
	v_pk_add_f32 v[80:81], v[54:55], v[34:35]
	v_pk_add_f32 v[34:35], v[54:55], v[34:35] neg_lo:[0,1] neg_hi:[0,1]
	v_pk_add_f32 v[92:93], v[84:85], v[80:81]
	v_pk_add_f32 v[80:81], v[84:85], v[80:81] neg_lo:[0,1] neg_hi:[0,1]
	v_pk_add_f32 v[84:85], v[58:59], v[34:35] op_sel:[0,1] op_sel_hi:[1,0] neg_hi:[0,1]
	v_pk_add_f32 v[34:35], v[58:59], v[34:35] op_sel:[0,1] op_sel_hi:[1,0] neg_lo:[0,1]
	v_pk_fma_f32 v[58:59], v[14:15], s[92:93], v[14:15] op_sel:[1,0,0] op_sel_hi:[0,1,1]
	v_pk_mul_f32 v[54:55], v[94:95], s[14:15] op_sel:[1,0] neg_lo:[1,0]
	v_pk_mul_f32 v[88:89], v[58:59], v[86:87] op_sel:[1,1] op_sel_hi:[0,1] neg_lo:[0,1]
	v_pk_fma_f32 v[54:55], v[94:95], s[42:43], v[54:55] op_sel_hi:[0,1,1]
	v_pk_fma_f32 v[86:87], v[58:59], v[86:87], v[88:89] op_sel_hi:[1,0,1]
	ds_write2_b64 v74, v[54:55], v[86:87] offset1:16
	v_pk_mul_f32 v[54:55], v[14:15], v[58:59] op_sel:[1,1] op_sel_hi:[0,1] neg_lo:[0,1]
	v_pk_fma_f32 v[54:55], v[14:15], v[58:59], v[54:55] op_sel_hi:[1,0,1]
	s_nop 0
	v_pk_mul_f32 v[58:59], v[54:55], v[102:103] op_sel:[1,1] op_sel_hi:[0,1] neg_lo:[0,1]
	v_pk_mul_f32 v[74:75], v[14:15], v[54:55] op_sel:[1,1] op_sel_hi:[0,1] neg_lo:[0,1]
	v_pk_fma_f32 v[58:59], v[54:55], v[102:103], v[58:59] op_sel_hi:[1,0,1]
	v_pk_fma_f32 v[54:55], v[14:15], v[54:55], v[74:75] op_sel_hi:[1,0,1]
	s_nop 0
	v_pk_mul_f32 v[74:75], v[54:55], v[56:57] op_sel:[1,1] op_sel_hi:[0,1] neg_lo:[0,1]
	v_pk_fma_f32 v[56:57], v[54:55], v[56:57], v[74:75] op_sel_hi:[1,0,1]
	ds_write2_b64 v73, v[58:59], v[56:57] offset0:32 offset1:48
	v_pk_mul_f32 v[56:57], v[14:15], v[54:55] op_sel:[1,1] op_sel_hi:[0,1] neg_lo:[0,1]
	v_pk_fma_f32 v[54:55], v[14:15], v[54:55], v[56:57] op_sel_hi:[1,0,1]
	s_nop 0
	v_pk_mul_f32 v[56:57], v[54:55], v[104:105] op_sel:[1,1] op_sel_hi:[0,1] neg_lo:[0,1]
	v_pk_mul_f32 v[58:59], v[14:15], v[54:55] op_sel:[1,1] op_sel_hi:[0,1] neg_lo:[0,1]
	v_pk_fma_f32 v[56:57], v[54:55], v[104:105], v[56:57] op_sel_hi:[1,0,1]
	v_pk_fma_f32 v[54:55], v[14:15], v[54:55], v[58:59] op_sel_hi:[1,0,1]
	s_nop 0
	v_pk_mul_f32 v[58:59], v[54:55], v[82:83] op_sel:[1,1] op_sel_hi:[0,1] neg_lo:[0,1]
	v_pk_fma_f32 v[58:59], v[54:55], v[82:83], v[58:59] op_sel_hi:[1,0,1]
	ds_write2_b64 v72, v[56:57], v[58:59] offset0:64 offset1:80
	v_pk_mul_f32 v[56:57], v[14:15], v[54:55] op_sel:[1,1] op_sel_hi:[0,1] neg_lo:[0,1]
	v_pk_fma_f32 v[54:55], v[14:15], v[54:55], v[56:57] op_sel_hi:[1,0,1]
	s_nop 0
	v_pk_mul_f32 v[56:57], v[54:55], v[98:99] op_sel:[1,1] op_sel_hi:[0,1] neg_lo:[0,1]
	v_pk_mul_f32 v[58:59], v[14:15], v[54:55] op_sel:[1,1] op_sel_hi:[0,1] neg_lo:[0,1]
	v_pk_fma_f32 v[56:57], v[54:55], v[98:99], v[56:57] op_sel_hi:[1,0,1]
	v_pk_fma_f32 v[54:55], v[14:15], v[54:55], v[58:59] op_sel_hi:[1,0,1]
	s_nop 0
	v_pk_mul_f32 v[58:59], v[54:55], v[92:93] op_sel:[1,1] op_sel_hi:[0,1] neg_lo:[0,1]
	v_pk_fma_f32 v[58:59], v[54:55], v[92:93], v[58:59] op_sel_hi:[1,0,1]
	ds_write2_b64 v71, v[56:57], v[58:59] offset0:96 offset1:112
	v_pk_mul_f32 v[56:57], v[14:15], v[54:55] op_sel:[1,1] op_sel_hi:[0,1] neg_lo:[0,1]
	v_pk_fma_f32 v[54:55], v[14:15], v[54:55], v[56:57] op_sel_hi:[1,0,1]
	s_nop 0
	v_pk_mul_f32 v[56:57], v[54:55], v[44:45] op_sel:[1,1] op_sel_hi:[0,1] neg_lo:[0,1]
	v_pk_fma_f32 v[44:45], v[54:55], v[44:45], v[56:57] op_sel_hi:[1,0,1]
	v_pk_mul_f32 v[56:57], v[14:15], v[54:55] op_sel:[1,1] op_sel_hi:[0,1] neg_lo:[0,1]
	v_pk_fma_f32 v[54:55], v[14:15], v[54:55], v[56:57] op_sel_hi:[1,0,1]
	s_nop 0
	v_pk_mul_f32 v[56:57], v[54:55], v[90:91] op_sel:[1,1] op_sel_hi:[0,1] neg_lo:[0,1]
	v_pk_fma_f32 v[56:57], v[54:55], v[90:91], v[56:57] op_sel_hi:[1,0,1]
	ds_write2_b64 v70, v[44:45], v[56:57] offset0:128 offset1:144
	v_pk_mul_f32 v[44:45], v[14:15], v[54:55] op_sel:[1,1] op_sel_hi:[0,1] neg_lo:[0,1]
	v_pk_fma_f32 v[44:45], v[14:15], v[54:55], v[44:45] op_sel_hi:[1,0,1]
	s_nop 0
	v_pk_mul_f32 v[54:55], v[44:45], v[48:49] op_sel:[1,1] op_sel_hi:[0,1] neg_lo:[0,1]
	v_pk_fma_f32 v[48:49], v[44:45], v[48:49], v[54:55] op_sel_hi:[1,0,1]
	v_pk_mul_f32 v[54:55], v[14:15], v[44:45] op_sel:[1,1] op_sel_hi:[0,1] neg_lo:[0,1]
	v_pk_fma_f32 v[44:45], v[14:15], v[44:45], v[54:55] op_sel_hi:[1,0,1]
	s_nop 0
	v_pk_mul_f32 v[54:55], v[44:45], v[52:53] op_sel:[1,1] op_sel_hi:[0,1] neg_lo:[0,1]
	v_pk_fma_f32 v[52:53], v[44:45], v[52:53], v[54:55] op_sel_hi:[1,0,1]
	ds_write2_b64 v69, v[48:49], v[52:53] offset0:160 offset1:176
	v_pk_mul_f32 v[48:49], v[14:15], v[44:45] op_sel:[1,1] op_sel_hi:[0,1] neg_lo:[0,1]
	v_pk_fma_f32 v[44:45], v[14:15], v[44:45], v[48:49] op_sel_hi:[1,0,1]
	s_nop 0
	v_pk_mul_f32 v[48:49], v[36:37], v[44:45] op_sel:[1,1] op_sel_hi:[1,0] neg_lo:[1,0]
	s_nop 0
	v_pk_fma_f32 v[36:37], v[36:37], v[44:45], v[48:49] op_sel_hi:[0,1,1]
	v_pk_mul_f32 v[48:49], v[14:15], v[44:45] op_sel:[1,1] op_sel_hi:[0,1] neg_lo:[0,1]
	v_pk_fma_f32 v[44:45], v[14:15], v[44:45], v[48:49] op_sel_hi:[1,0,1]
	s_nop 0
	v_pk_mul_f32 v[48:49], v[44:45], v[76:77] op_sel:[1,1] op_sel_hi:[0,1] neg_lo:[0,1]
	v_pk_fma_f32 v[48:49], v[44:45], v[76:77], v[48:49] op_sel_hi:[1,0,1]
	ds_write2_b64 v68, v[36:37], v[48:49] offset0:192 offset1:208
	v_pk_mul_f32 v[36:37], v[14:15], v[44:45] op_sel:[1,1] op_sel_hi:[0,1] neg_lo:[0,1]
	v_pk_fma_f32 v[36:37], v[14:15], v[44:45], v[36:37] op_sel_hi:[1,0,1]
	s_nop 0
	v_pk_mul_f32 v[44:45], v[40:41], v[36:37] op_sel:[1,1] op_sel_hi:[1,0] neg_lo:[1,0]
	s_nop 0
	v_pk_fma_f32 v[40:41], v[40:41], v[36:37], v[44:45] op_sel_hi:[0,1,1]
	v_pk_mul_f32 v[44:45], v[14:15], v[36:37] op_sel:[1,1] op_sel_hi:[0,1] neg_lo:[0,1]
	v_pk_fma_f32 v[36:37], v[14:15], v[36:37], v[44:45] op_sel_hi:[1,0,1]
	s_nop 0
	v_pk_mul_f32 v[44:45], v[36:37], v[84:85] op_sel:[1,1] op_sel_hi:[0,1] neg_lo:[0,1]
	v_pk_fma_f32 v[44:45], v[36:37], v[84:85], v[44:45] op_sel_hi:[1,0,1]
	ds_write2_b64 v67, v[40:41], v[44:45] offset0:224 offset1:240
	v_pk_mul_f32 v[40:41], v[14:15], v[36:37] op_sel:[1,1] op_sel_hi:[0,1] neg_lo:[0,1]
	v_pk_fma_f32 v[36:37], v[14:15], v[36:37], v[40:41] op_sel_hi:[1,0,1]
	s_nop 0
	v_pk_mul_f32 v[40:41], v[28:29], v[36:37] op_sel:[1,1] op_sel_hi:[1,0] neg_lo:[1,0]
	s_nop 0
	v_pk_fma_f32 v[28:29], v[28:29], v[36:37], v[40:41] op_sel_hi:[0,1,1]
	v_pk_mul_f32 v[40:41], v[14:15], v[36:37] op_sel:[1,1] op_sel_hi:[0,1] neg_lo:[0,1]
	v_pk_fma_f32 v[36:37], v[14:15], v[36:37], v[40:41] op_sel_hi:[1,0,1]
	s_nop 0
	v_pk_mul_f32 v[40:41], v[78:79], v[36:37] op_sel:[1,1] op_sel_hi:[1,0] neg_lo:[1,0]
	s_nop 0
	v_pk_fma_f32 v[40:41], v[78:79], v[36:37], v[40:41] op_sel_hi:[0,1,1]
	ds_write2_b64 v66, v[28:29], v[40:41] offset1:16
	v_pk_mul_f32 v[28:29], v[14:15], v[36:37] op_sel:[1,1] op_sel_hi:[0,1] neg_lo:[0,1]
	v_pk_fma_f32 v[28:29], v[14:15], v[36:37], v[28:29] op_sel_hi:[1,0,1]
	s_nop 0
	v_pk_mul_f32 v[36:37], v[32:33], v[28:29] op_sel:[1,1] op_sel_hi:[1,0] neg_lo:[1,0]
	s_nop 0
	v_pk_fma_f32 v[32:33], v[32:33], v[28:29], v[36:37] op_sel_hi:[0,1,1]
	v_pk_mul_f32 v[36:37], v[14:15], v[28:29] op_sel:[1,1] op_sel_hi:[0,1] neg_lo:[0,1]
	v_pk_fma_f32 v[28:29], v[14:15], v[28:29], v[36:37] op_sel_hi:[1,0,1]
	s_nop 0
	v_pk_mul_f32 v[36:37], v[50:51], v[28:29] op_sel:[1,1] op_sel_hi:[1,0] neg_lo:[1,0]
	s_nop 0
	v_pk_fma_f32 v[36:37], v[50:51], v[28:29], v[36:37] op_sel_hi:[0,1,1]
	ds_write2_b64 v65, v[32:33], v[36:37] offset0:32 offset1:48
	v_pk_mul_f32 v[32:33], v[14:15], v[28:29] op_sel:[1,1] op_sel_hi:[0,1] neg_lo:[0,1]
	v_pk_fma_f32 v[28:29], v[14:15], v[28:29], v[32:33] op_sel_hi:[1,0,1]
	s_nop 0
	v_pk_mul_f32 v[32:33], v[24:25], v[28:29] op_sel:[1,1] op_sel_hi:[1,0] neg_lo:[1,0]
	s_nop 0
	v_pk_fma_f32 v[24:25], v[24:25], v[28:29], v[32:33] op_sel_hi:[0,1,1]
	v_pk_mul_f32 v[32:33], v[14:15], v[28:29] op_sel:[1,1] op_sel_hi:[0,1] neg_lo:[0,1]
	v_pk_fma_f32 v[28:29], v[14:15], v[28:29], v[32:33] op_sel_hi:[1,0,1]
	s_nop 0
	v_pk_mul_f32 v[32:33], v[46:47], v[28:29] op_sel:[1,1] op_sel_hi:[1,0] neg_lo:[1,0]
	s_nop 0
	v_pk_fma_f32 v[32:33], v[46:47], v[28:29], v[32:33] op_sel_hi:[0,1,1]
	ds_write2_b64 v64, v[24:25], v[32:33] offset0:64 offset1:80
	v_pk_mul_f32 v[24:25], v[14:15], v[28:29] op_sel:[1,1] op_sel_hi:[0,1] neg_lo:[0,1]
	v_pk_fma_f32 v[24:25], v[14:15], v[28:29], v[24:25] op_sel_hi:[1,0,1]
	s_nop 0
	v_pk_mul_f32 v[28:29], v[26:27], v[24:25] op_sel:[1,1] op_sel_hi:[1,0] neg_lo:[1,0]
	s_nop 0
	v_pk_fma_f32 v[26:27], v[26:27], v[24:25], v[28:29] op_sel_hi:[0,1,1]
	v_pk_mul_f32 v[28:29], v[14:15], v[24:25] op_sel:[1,1] op_sel_hi:[0,1] neg_lo:[0,1]
	v_pk_fma_f32 v[24:25], v[14:15], v[24:25], v[28:29] op_sel_hi:[1,0,1]
	s_nop 0
	v_pk_mul_f32 v[28:29], v[80:81], v[24:25] op_sel:[1,1] op_sel_hi:[1,0] neg_lo:[1,0]
	s_nop 0
	v_pk_fma_f32 v[28:29], v[80:81], v[24:25], v[28:29] op_sel_hi:[0,1,1]
	ds_write2_b64 v63, v[26:27], v[28:29] offset0:96 offset1:112
	v_pk_mul_f32 v[26:27], v[14:15], v[24:25] op_sel:[1,1] op_sel_hi:[0,1] neg_lo:[0,1]
	v_pk_fma_f32 v[24:25], v[14:15], v[24:25], v[26:27] op_sel_hi:[1,0,1]
	s_nop 0
	v_pk_mul_f32 v[26:27], v[20:21], v[24:25] op_sel:[1,1] op_sel_hi:[1,0] neg_lo:[1,0]
	s_nop 0
	v_pk_fma_f32 v[20:21], v[20:21], v[24:25], v[26:27] op_sel_hi:[0,1,1]
	v_pk_mul_f32 v[26:27], v[14:15], v[24:25] op_sel:[1,1] op_sel_hi:[0,1] neg_lo:[0,1]
	v_pk_fma_f32 v[24:25], v[14:15], v[24:25], v[26:27] op_sel_hi:[1,0,1]
	s_nop 0
	v_pk_mul_f32 v[26:27], v[38:39], v[24:25] op_sel:[1,1] op_sel_hi:[1,0] neg_lo:[1,0]
	s_nop 0
	v_pk_fma_f32 v[26:27], v[38:39], v[24:25], v[26:27] op_sel_hi:[0,1,1]
	ds_write2_b64 v62, v[20:21], v[26:27] offset0:128 offset1:144
	v_pk_mul_f32 v[20:21], v[14:15], v[24:25] op_sel:[1,1] op_sel_hi:[0,1] neg_lo:[0,1]
	v_pk_fma_f32 v[20:21], v[14:15], v[24:25], v[20:21] op_sel_hi:[1,0,1]
	s_nop 0
	v_pk_mul_f32 v[24:25], v[22:23], v[20:21] op_sel:[1,1] op_sel_hi:[1,0] neg_lo:[1,0]
	s_nop 0
	v_pk_fma_f32 v[22:23], v[22:23], v[20:21], v[24:25] op_sel_hi:[0,1,1]
	v_pk_mul_f32 v[24:25], v[14:15], v[20:21] op_sel:[1,1] op_sel_hi:[0,1] neg_lo:[0,1]
	v_pk_fma_f32 v[20:21], v[14:15], v[20:21], v[24:25] op_sel_hi:[1,0,1]
	s_nop 0
	v_pk_mul_f32 v[24:25], v[42:43], v[20:21] op_sel:[1,1] op_sel_hi:[1,0] neg_lo:[1,0]
	s_nop 0
	v_pk_fma_f32 v[24:25], v[42:43], v[20:21], v[24:25] op_sel_hi:[0,1,1]
	ds_write2_b64 v61, v[22:23], v[24:25] offset0:160 offset1:176
	v_pk_mul_f32 v[22:23], v[14:15], v[20:21] op_sel:[1,1] op_sel_hi:[0,1] neg_lo:[0,1]
	v_pk_fma_f32 v[20:21], v[14:15], v[20:21], v[22:23] op_sel_hi:[1,0,1]
	s_nop 0
	v_pk_mul_f32 v[22:23], v[16:17], v[20:21] op_sel:[1,1] op_sel_hi:[1,0] neg_lo:[1,0]
	s_nop 0
	v_pk_fma_f32 v[16:17], v[16:17], v[20:21], v[22:23] op_sel_hi:[0,1,1]
	v_pk_mul_f32 v[22:23], v[14:15], v[20:21] op_sel:[1,1] op_sel_hi:[0,1] neg_lo:[0,1]
	v_pk_fma_f32 v[20:21], v[14:15], v[20:21], v[22:23] op_sel_hi:[1,0,1]
	s_nop 0
	v_pk_mul_f32 v[22:23], v[30:31], v[20:21] op_sel:[1,1] op_sel_hi:[1,0] neg_lo:[1,0]
	s_nop 0
	v_pk_fma_f32 v[22:23], v[30:31], v[20:21], v[22:23] op_sel_hi:[0,1,1]
	ds_write2_b64 v60, v[16:17], v[22:23] offset0:192 offset1:208
	v_pk_mul_f32 v[16:17], v[14:15], v[20:21] op_sel:[1,1] op_sel_hi:[0,1] neg_lo:[0,1]
	v_pk_fma_f32 v[16:17], v[14:15], v[20:21], v[16:17] op_sel_hi:[1,0,1]
	s_nop 0
	v_pk_mul_f32 v[20:21], v[18:19], v[16:17] op_sel:[1,1] op_sel_hi:[1,0] neg_lo:[1,0]
	s_nop 0
	v_pk_fma_f32 v[18:19], v[18:19], v[16:17], v[20:21] op_sel_hi:[0,1,1]
	v_pk_mul_f32 v[20:21], v[14:15], v[16:17] op_sel:[1,1] op_sel_hi:[0,1] neg_lo:[0,1]
	v_pk_fma_f32 v[14:15], v[14:15], v[16:17], v[20:21] op_sel_hi:[1,0,1]
	s_nop 0
	v_pk_mul_f32 v[16:17], v[34:35], v[14:15] op_sel:[1,1] op_sel_hi:[1,0] neg_lo:[1,0]
	s_nop 0
	v_pk_fma_f32 v[14:15], v[34:35], v[14:15], v[16:17] op_sel_hi:[0,1,1]
	ds_write2_b64 v13, v[18:19], v[14:15] offset0:224 offset1:240
	v_mov_b32_e32 v14, v1
	v_mov_b32_e32 v10, v178
	v_mov_b32_e32 v13, v177
	s_waitcnt lgkmcnt(0)
	s_barrier
	v_mov_b32_e32 v48, v168
	v_xor_b32_e32 v16, 1, v13
	v_lshlrev_b32_e32 v10, 3, v10
	v_lshlrev_b32_e32 v16, 3, v16
	v_add3_u32 v18, 0, v16, v10
	v_xor_b32_e32 v16, 2, v13
	v_lshlrev_b32_e32 v16, 3, v16
	v_xor_b32_e32 v24, 5, v13
	v_add3_u32 v20, 0, v16, v10
	v_xor_b32_e32 v16, 3, v13
	v_lshlrev_b32_e32 v24, 3, v24
	v_lshlrev_b32_e32 v15, 3, v13
	v_lshlrev_b32_e32 v16, 3, v16
	v_add3_u32 v26, 0, v24, v10
	v_xor_b32_e32 v24, 6, v13
	v_add3_u32 v15, 0, v15, v10
	v_add3_u32 v22, 0, v16, v10
	v_lshlrev_b32_e32 v24, 3, v24
	v_xor_b32_e32 v32, 9, v13
	ds_read_b64 v[16:17], v15
	ds_read_b64 v[18:19], v18
	ds_read_b64 v[20:21], v20
	ds_read_b64 v[22:23], v22
	v_xor_b32_e32 v15, 4, v13
	v_add3_u32 v28, 0, v24, v10
	v_xor_b32_e32 v24, 7, v13
	v_lshlrev_b32_e32 v32, 3, v32
	v_lshlrev_b32_e32 v15, 3, v15
	v_lshlrev_b32_e32 v24, 3, v24
	v_add3_u32 v34, 0, v32, v10
	v_xor_b32_e32 v32, 10, v13
	v_add3_u32 v15, 0, v15, v10
	v_add3_u32 v30, 0, v24, v10
	v_lshlrev_b32_e32 v32, 3, v32
	ds_read_b64 v[24:25], v15
	ds_read_b64 v[26:27], v26
	ds_read_b64 v[28:29], v28
	ds_read_b64 v[30:31], v30
	v_xor_b32_e32 v15, 8, v13
	v_add3_u32 v36, 0, v32, v10
	v_xor_b32_e32 v32, 11, v13
	v_lshlrev_b32_e32 v15, 3, v15
	v_lshlrev_b32_e32 v32, 3, v32
	v_xor_b32_e32 v40, 13, v13
	v_add3_u32 v15, 0, v15, v10
	v_add3_u32 v38, 0, v32, v10
	v_lshlrev_b32_e32 v40, 3, v40
	ds_read_b64 v[32:33], v15
	ds_read_b64 v[34:35], v34
	ds_read_b64 v[36:37], v36
	ds_read_b64 v[38:39], v38
	v_xor_b32_e32 v15, 12, v13
	v_add3_u32 v42, 0, v40, v10
	v_xor_b32_e32 v40, 14, v13
	v_xor_b32_e32 v13, 15, v13
	v_lshlrev_b32_e32 v15, 3, v15
	v_lshlrev_b32_e32 v40, 3, v40
	v_lshlrev_b32_e32 v13, 3, v13
	v_add3_u32 v15, 0, v15, v10
	v_add3_u32 v44, 0, v40, v10
	v_add3_u32 v10, 0, v13, v10
	ds_read_b64 v[40:41], v15
	ds_read_b64 v[42:43], v42
	ds_read_b64 v[44:45], v44
	ds_read_b64 v[46:47], v10
	s_waitcnt lgkmcnt(7)
	v_pk_add_f32 v[52:53], v[16:17], v[32:33]
	v_mov_b32_e32 v10, v166
	v_pk_add_f32 v[16:17], v[16:17], v[32:33] neg_lo:[0,1] neg_hi:[0,1]
	s_waitcnt lgkmcnt(6)
	v_pk_add_f32 v[32:33], v[18:19], v[34:35]
	v_pk_add_f32 v[18:19], v[18:19], v[34:35] neg_lo:[0,1] neg_hi:[0,1]
	v_mov_b32_e32 v50, v170
	v_ashrrev_i32_e32 v15, 31, v14
	v_pk_mul_f32 v[34:35], v[18:19], v[50:51] op_sel:[1,0] op_sel_hi:[0,0] neg_lo:[1,1] neg_hi:[0,1]
	v_pk_fma_f32 v[18:19], v[18:19], v[10:11], v[34:35] op_sel_hi:[1,0,1]
	s_waitcnt lgkmcnt(5)
	v_pk_add_f32 v[34:35], v[20:21], v[36:37]
	v_pk_add_f32 v[20:21], v[20:21], v[36:37] neg_lo:[0,1] neg_hi:[0,1]
	s_mov_b32 s39, 0x8000
	v_pk_mul_f32 v[36:37], v[20:21], v[48:49] op_sel:[1,0] op_sel_hi:[0,0] neg_lo:[1,1] neg_hi:[0,1]
	v_pk_fma_f32 v[20:21], v[20:21], v[48:49], v[36:37] op_sel_hi:[1,0,1]
	s_waitcnt lgkmcnt(4)
	v_pk_add_f32 v[36:37], v[22:23], v[38:39]
	v_pk_add_f32 v[22:23], v[22:23], v[38:39] neg_lo:[0,1] neg_hi:[0,1]
	s_nop 0
	v_pk_mul_f32 v[38:39], v[22:23], v[50:51] op_sel_hi:[1,0]
	s_nop 0
	v_pk_fma_f32 v[22:23], v[22:23], v[10:11], v[38:39] op_sel:[1,0,0] op_sel_hi:[0,0,1] neg_lo:[1,1,0] neg_hi:[0,1,0]
	s_waitcnt lgkmcnt(3)
	v_pk_add_f32 v[38:39], v[24:25], v[40:41]
	v_pk_add_f32 v[24:25], v[24:25], v[40:41] neg_lo:[0,1] neg_hi:[0,1]
	v_mov_b32_e32 v13, v177
	v_xor_b32_e32 v41, 0x80000000, v24
	v_mov_b32_e32 v40, v25
	s_waitcnt lgkmcnt(2)
	v_pk_add_f32 v[24:25], v[26:27], v[42:43]
	v_pk_add_f32 v[26:27], v[26:27], v[42:43] neg_lo:[0,1] neg_hi:[0,1]
	s_nop 0
	v_pk_mul_f32 v[42:43], v[26:27], v[50:51] op_sel_hi:[1,0] neg_lo:[0,1] neg_hi:[0,1]
	s_nop 0
	v_pk_fma_f32 v[26:27], v[26:27], v[10:11], v[42:43] op_sel:[1,0,0] op_sel_hi:[0,0,1] neg_lo:[1,1,0] neg_hi:[0,1,0]
	s_waitcnt lgkmcnt(1)
	v_pk_add_f32 v[42:43], v[28:29], v[44:45]
	v_pk_add_f32 v[28:29], v[28:29], v[44:45] neg_lo:[0,1] neg_hi:[0,1]
	s_nop 0
	v_pk_mul_f32 v[44:45], v[28:29], v[48:49] op_sel:[1,0] op_sel_hi:[0,0] neg_lo:[1,1] neg_hi:[0,1]
	s_nop 0
	v_pk_fma_f32 v[28:29], v[28:29], v[48:49], v[44:45] op_sel_hi:[1,0,1] neg_lo:[0,1,0] neg_hi:[0,1,0]
	s_waitcnt lgkmcnt(0)
	v_pk_add_f32 v[44:45], v[30:31], v[46:47]
	v_pk_add_f32 v[30:31], v[30:31], v[46:47] neg_lo:[0,1] neg_hi:[0,1]
	s_nop 0
	v_pk_mul_f32 v[46:47], v[30:31], v[50:51] op_sel:[1,0] op_sel_hi:[0,0] neg_lo:[1,1] neg_hi:[0,1]
	v_pk_add_f32 v[50:51], v[32:33], v[24:25]
	v_pk_add_f32 v[24:25], v[32:33], v[24:25] neg_lo:[0,1] neg_hi:[0,1]
	v_pk_fma_f32 v[30:31], v[30:31], v[10:11], v[46:47] op_sel_hi:[1,0,1] neg_lo:[0,1,0] neg_hi:[0,1,0]
	v_pk_mul_f32 v[32:33], v[24:25], v[48:49] op_sel:[1,0] op_sel_hi:[0,0] neg_lo:[1,1] neg_hi:[0,1]
	v_pk_add_f32 v[46:47], v[52:53], v[38:39]
	v_pk_fma_f32 v[24:25], v[24:25], v[48:49], v[32:33] op_sel_hi:[1,0,1]
	v_pk_add_f32 v[32:33], v[34:35], v[42:43]
	v_pk_add_f32 v[34:35], v[34:35], v[42:43] neg_lo:[0,1] neg_hi:[0,1]
	v_pk_add_f32 v[38:39], v[52:53], v[38:39] neg_lo:[0,1] neg_hi:[0,1]
	v_xor_b32_e32 v43, 0x80000000, v34
	v_mov_b32_e32 v42, v35
	v_pk_add_f32 v[34:35], v[36:37], v[44:45]
	v_pk_add_f32 v[36:37], v[36:37], v[44:45] neg_lo:[0,1] neg_hi:[0,1]
	v_mov_b32_e32 v10, v179
	v_pk_mul_f32 v[44:45], v[36:37], v[48:49] op_sel:[1,0] op_sel_hi:[0,0] neg_lo:[1,1] neg_hi:[0,1]
	s_nop 0
	v_pk_fma_f32 v[36:37], v[36:37], v[48:49], v[44:45] op_sel_hi:[1,0,1] neg_lo:[0,1,0] neg_hi:[0,1,0]
	v_pk_add_f32 v[44:45], v[46:47], v[32:33]
	v_pk_add_f32 v[32:33], v[46:47], v[32:33] neg_lo:[0,1] neg_hi:[0,1]
	v_pk_add_f32 v[46:47], v[50:51], v[34:35]
	v_pk_add_f32 v[34:35], v[50:51], v[34:35] neg_lo:[0,1] neg_hi:[0,1]
	s_nop 0
	v_xor_b32_e32 v51, 0x80000000, v34
	v_mov_b32_e32 v50, v35
	v_pk_add_f32 v[34:35], v[44:45], v[46:47]
	v_pk_add_f32 v[44:45], v[44:45], v[46:47] neg_lo:[0,1] neg_hi:[0,1]
	v_pk_add_f32 v[46:47], v[32:33], v[50:51]
	v_pk_add_f32 v[32:33], v[32:33], v[50:51] neg_lo:[0,1] neg_hi:[0,1]
	v_pk_add_f32 v[50:51], v[38:39], v[42:43]
	v_pk_add_f32 v[38:39], v[38:39], v[42:43] neg_lo:[0,1] neg_hi:[0,1]
	v_pk_add_f32 v[42:43], v[24:25], v[36:37]
	v_pk_add_f32 v[24:25], v[24:25], v[36:37] neg_lo:[0,1] neg_hi:[0,1]
	s_nop 0
	v_xor_b32_e32 v37, 0x80000000, v24
	v_mov_b32_e32 v36, v25
	v_pk_add_f32 v[24:25], v[50:51], v[42:43]
	v_pk_add_f32 v[42:43], v[50:51], v[42:43] neg_lo:[0,1] neg_hi:[0,1]
	v_pk_add_f32 v[50:51], v[38:39], v[36:37]
	v_pk_add_f32 v[36:37], v[38:39], v[36:37] neg_lo:[0,1] neg_hi:[0,1]
	v_pk_add_f32 v[38:39], v[16:17], v[40:41]
	v_pk_add_f32 v[16:17], v[16:17], v[40:41] neg_lo:[0,1] neg_hi:[0,1]
	v_pk_add_f32 v[40:41], v[18:19], v[26:27]
	v_pk_add_f32 v[18:19], v[18:19], v[26:27] neg_lo:[0,1] neg_hi:[0,1]
	s_nop 0
	v_pk_mul_f32 v[26:27], v[48:49], v[18:19] op_sel:[0,1] op_sel_hi:[0,0] neg_lo:[1,1] neg_hi:[1,0]
	v_pk_fma_f32 v[18:19], v[48:49], v[18:19], v[26:27] op_sel_hi:[0,1,1]
	v_pk_add_f32 v[26:27], v[20:21], v[28:29]
	v_pk_add_f32 v[20:21], v[20:21], v[28:29] neg_lo:[0,1] neg_hi:[0,1]
	s_nop 0
	v_xor_b32_e32 v29, 0x80000000, v20
	v_mov_b32_e32 v28, v21
	v_pk_add_f32 v[20:21], v[22:23], v[30:31]
	v_pk_add_f32 v[22:23], v[22:23], v[30:31] neg_lo:[0,1] neg_hi:[0,1]
	s_nop 0
	v_pk_mul_f32 v[30:31], v[48:49], v[22:23] op_sel:[0,1] op_sel_hi:[0,0] neg_lo:[1,1] neg_hi:[1,0]
	v_pk_fma_f32 v[22:23], v[48:49], v[22:23], v[30:31] op_sel_hi:[0,1,1] neg_lo:[1,0,0] neg_hi:[1,0,0]
	v_pk_add_f32 v[30:31], v[38:39], v[26:27]
	v_pk_add_f32 v[26:27], v[38:39], v[26:27] neg_lo:[0,1] neg_hi:[0,1]
	v_pk_add_f32 v[38:39], v[40:41], v[20:21]
	v_pk_add_f32 v[20:21], v[40:41], v[20:21] neg_lo:[0,1] neg_hi:[0,1]
	v_mov_b32_e32 v48, v168
	v_xor_b32_e32 v41, 0x80000000, v20
	v_mov_b32_e32 v40, v21
	v_pk_add_f32 v[20:21], v[30:31], v[38:39]
	v_pk_add_f32 v[30:31], v[30:31], v[38:39] neg_lo:[0,1] neg_hi:[0,1]
	v_pk_add_f32 v[38:39], v[26:27], v[40:41]
	v_pk_add_f32 v[26:27], v[26:27], v[40:41] neg_lo:[0,1] neg_hi:[0,1]
	v_pk_add_f32 v[40:41], v[16:17], v[28:29]
	v_pk_add_f32 v[16:17], v[16:17], v[28:29] neg_lo:[0,1] neg_hi:[0,1]
	v_pk_add_f32 v[28:29], v[18:19], v[22:23]
	v_pk_add_f32 v[18:19], v[18:19], v[22:23] neg_lo:[0,1] neg_hi:[0,1]
	s_nop 0
	v_xor_b32_e32 v23, 0x80000000, v18
	v_mov_b32_e32 v22, v19
	v_pk_add_f32 v[18:19], v[40:41], v[28:29]
	v_pk_add_f32 v[28:29], v[40:41], v[28:29] neg_lo:[0,1] neg_hi:[0,1]
	v_pk_add_f32 v[40:41], v[16:17], v[22:23]
	v_pk_add_f32 v[16:17], v[16:17], v[22:23] neg_lo:[0,1] neg_hi:[0,1]
	v_lshl_add_u64 v[22:23], v[14:15], 3, s[48:49]
	global_store_dwordx2 v[22:23], v[34:35], off
	v_add_u32_e32 v22, 0x200, v14
	v_ashrrev_i32_e32 v23, 31, v22
	v_lshl_add_u64 v[22:23], v[22:23], 3, s[48:49]
	global_store_dwordx2 v[22:23], v[20:21], off
	v_add_u32_e32 v20, 0x400, v14
	v_ashrrev_i32_e32 v21, 31, v20
	v_lshl_add_u64 v[20:21], v[20:21], 3, s[48:49]
	global_store_dwordx2 v[20:21], v[24:25], off
	v_add_u32_e32 v20, 0x600, v14
	v_ashrrev_i32_e32 v21, 31, v20
	v_lshl_add_u64 v[20:21], v[20:21], 3, s[48:49]
	global_store_dwordx2 v[20:21], v[18:19], off
	v_add_u32_e32 v18, 0x800, v14
	v_ashrrev_i32_e32 v19, 31, v18
	v_lshl_add_u64 v[18:19], v[18:19], 3, s[48:49]
	global_store_dwordx2 v[18:19], v[46:47], off
	v_add_u32_e32 v18, 0xa00, v14
	v_ashrrev_i32_e32 v19, 31, v18
	v_lshl_add_u64 v[18:19], v[18:19], 3, s[48:49]
	global_store_dwordx2 v[18:19], v[38:39], off
	v_add_u32_e32 v18, 0xc00, v14
	v_ashrrev_i32_e32 v19, 31, v18
	v_lshl_add_u64 v[18:19], v[18:19], 3, s[48:49]
	global_store_dwordx2 v[18:19], v[50:51], off
	v_add_u32_e32 v18, 0xe00, v14
	v_ashrrev_i32_e32 v19, 31, v18
	v_lshl_add_u64 v[18:19], v[18:19], 3, s[48:49]
	global_store_dwordx2 v[18:19], v[40:41], off
	v_add_u32_e32 v18, 0x1000, v14
	v_ashrrev_i32_e32 v19, 31, v18
	v_lshl_add_u64 v[18:19], v[18:19], 3, s[48:49]
	global_store_dwordx2 v[18:19], v[44:45], off
	v_add_u32_e32 v18, 0x1200, v14
	v_ashrrev_i32_e32 v19, 31, v18
	v_lshl_add_u64 v[18:19], v[18:19], 3, s[48:49]
	global_store_dwordx2 v[18:19], v[30:31], off
	v_add_u32_e32 v18, 0x1400, v14
	v_ashrrev_i32_e32 v19, 31, v18
	v_lshl_add_u64 v[18:19], v[18:19], 3, s[48:49]
	global_store_dwordx2 v[18:19], v[42:43], off
	v_add_u32_e32 v18, 0x1600, v14
	v_ashrrev_i32_e32 v19, 31, v18
	v_lshl_add_u64 v[18:19], v[18:19], 3, s[48:49]
	global_store_dwordx2 v[18:19], v[28:29], off
	v_add_u32_e32 v18, 0x1800, v14
	v_ashrrev_i32_e32 v19, 31, v18
	v_lshl_add_u64 v[18:19], v[18:19], 3, s[48:49]
	global_store_dwordx2 v[18:19], v[32:33], off
	v_add_u32_e32 v18, 0x1a00, v14
	v_ashrrev_i32_e32 v19, 31, v18
	v_lshl_add_u64 v[18:19], v[18:19], 3, s[48:49]
	global_store_dwordx2 v[18:19], v[26:27], off
	v_add_u32_e32 v18, 0x1c00, v14
	v_ashrrev_i32_e32 v19, 31, v18
	v_lshl_add_u64 v[18:19], v[18:19], 3, s[48:49]
	global_store_dwordx2 v[18:19], v[36:37], off
	v_add_u32_e32 v18, 0x1e00, v14
	v_ashrrev_i32_e32 v19, 31, v18
	v_lshl_add_u64 v[18:19], v[18:19], 3, s[48:49]
	global_store_dwordx2 v[18:19], v[16:17], off
	v_mov_b32_e32 v50, v170
	v_xor_b32_e32 v16, 1, v13
	v_lshlrev_b32_e32 v10, 3, v10
	v_lshlrev_b32_e32 v16, 3, v16
	v_add3_u32 v18, 0, v16, v10
	v_xor_b32_e32 v16, 2, v13
	v_lshlrev_b32_e32 v16, 3, v16
	v_xor_b32_e32 v24, 5, v13
	v_add3_u32 v20, 0, v16, v10
	v_xor_b32_e32 v16, 3, v13
	v_lshlrev_b32_e32 v24, 3, v24
	v_lshlrev_b32_e32 v15, 3, v13
	v_lshlrev_b32_e32 v16, 3, v16
	v_add3_u32 v26, 0, v24, v10
	v_xor_b32_e32 v24, 6, v13
	v_add3_u32 v15, 0, v15, v10
	v_add3_u32 v22, 0, v16, v10
	v_lshlrev_b32_e32 v24, 3, v24
	v_xor_b32_e32 v32, 9, v13
	ds_read_b64 v[16:17], v15
	ds_read_b64 v[18:19], v18
	ds_read_b64 v[20:21], v20
	ds_read_b64 v[22:23], v22
	v_xor_b32_e32 v15, 4, v13
	v_add3_u32 v28, 0, v24, v10
	v_xor_b32_e32 v24, 7, v13
	v_lshlrev_b32_e32 v32, 3, v32
	v_lshlrev_b32_e32 v15, 3, v15
	v_lshlrev_b32_e32 v24, 3, v24
	v_add3_u32 v34, 0, v32, v10
	v_xor_b32_e32 v32, 10, v13
	v_add3_u32 v15, 0, v15, v10
	v_add3_u32 v30, 0, v24, v10
	v_lshlrev_b32_e32 v32, 3, v32
	ds_read_b64 v[24:25], v15
	ds_read_b64 v[26:27], v26
	ds_read_b64 v[28:29], v28
	ds_read_b64 v[30:31], v30
	v_xor_b32_e32 v15, 8, v13
	v_add3_u32 v36, 0, v32, v10
	v_xor_b32_e32 v32, 11, v13
	v_lshlrev_b32_e32 v15, 3, v15
	v_lshlrev_b32_e32 v32, 3, v32
	v_xor_b32_e32 v40, 13, v13
	v_add3_u32 v15, 0, v15, v10
	v_add3_u32 v38, 0, v32, v10
	v_lshlrev_b32_e32 v40, 3, v40
	ds_read_b64 v[32:33], v15
	ds_read_b64 v[34:35], v34
	ds_read_b64 v[36:37], v36
	ds_read_b64 v[38:39], v38
	v_xor_b32_e32 v15, 12, v13
	v_add3_u32 v42, 0, v40, v10
	v_xor_b32_e32 v40, 14, v13
	v_xor_b32_e32 v13, 15, v13
	v_lshlrev_b32_e32 v15, 3, v15
	v_lshlrev_b32_e32 v40, 3, v40
	v_lshlrev_b32_e32 v13, 3, v13
	v_add3_u32 v15, 0, v15, v10
	v_add3_u32 v44, 0, v40, v10
	v_add3_u32 v10, 0, v13, v10
	ds_read_b64 v[40:41], v15
	ds_read_b64 v[42:43], v42
	ds_read_b64 v[44:45], v44
	ds_read_b64 v[46:47], v10
	s_waitcnt lgkmcnt(7)
	v_pk_add_f32 v[52:53], v[16:17], v[32:33]
	v_mov_b32_e32 v10, v166
	v_pk_add_f32 v[16:17], v[16:17], v[32:33] neg_lo:[0,1] neg_hi:[0,1]
	s_waitcnt lgkmcnt(6)
	v_pk_add_f32 v[32:33], v[18:19], v[34:35]
	v_pk_add_f32 v[18:19], v[18:19], v[34:35] neg_lo:[0,1] neg_hi:[0,1]
	s_nop 0
	v_pk_mul_f32 v[34:35], v[18:19], v[50:51] op_sel:[1,0] op_sel_hi:[0,0] neg_lo:[1,1] neg_hi:[0,1]
	v_pk_fma_f32 v[18:19], v[18:19], v[10:11], v[34:35] op_sel_hi:[1,0,1]
	s_waitcnt lgkmcnt(5)
	v_pk_add_f32 v[34:35], v[20:21], v[36:37]
	v_pk_add_f32 v[20:21], v[20:21], v[36:37] neg_lo:[0,1] neg_hi:[0,1]
	s_nop 0
	v_pk_mul_f32 v[36:37], v[20:21], v[48:49] op_sel:[1,0] op_sel_hi:[0,0] neg_lo:[1,1] neg_hi:[0,1]
	v_pk_fma_f32 v[20:21], v[20:21], v[48:49], v[36:37] op_sel_hi:[1,0,1]
	s_waitcnt lgkmcnt(4)
	v_pk_add_f32 v[36:37], v[22:23], v[38:39]
	v_pk_add_f32 v[22:23], v[22:23], v[38:39] neg_lo:[0,1] neg_hi:[0,1]
	s_nop 0
	v_pk_mul_f32 v[38:39], v[22:23], v[50:51] op_sel_hi:[1,0]
	s_nop 0
	v_pk_fma_f32 v[22:23], v[22:23], v[10:11], v[38:39] op_sel:[1,0,0] op_sel_hi:[0,0,1] neg_lo:[1,1,0] neg_hi:[0,1,0]
	s_waitcnt lgkmcnt(3)
	v_pk_add_f32 v[38:39], v[24:25], v[40:41]
	v_pk_add_f32 v[24:25], v[24:25], v[40:41] neg_lo:[0,1] neg_hi:[0,1]
	v_mov_b32_e32 v13, v174
	v_xor_b32_e32 v41, 0x80000000, v24
	v_mov_b32_e32 v40, v25
	s_waitcnt lgkmcnt(2)
	v_pk_add_f32 v[24:25], v[26:27], v[42:43]
	v_pk_add_f32 v[26:27], v[26:27], v[42:43] neg_lo:[0,1] neg_hi:[0,1]
	s_nop 0
	v_pk_mul_f32 v[42:43], v[26:27], v[50:51] op_sel_hi:[1,0] neg_lo:[0,1] neg_hi:[0,1]
	s_nop 0
	v_pk_fma_f32 v[26:27], v[26:27], v[10:11], v[42:43] op_sel:[1,0,0] op_sel_hi:[0,0,1] neg_lo:[1,1,0] neg_hi:[0,1,0]
	s_waitcnt lgkmcnt(1)
	v_pk_add_f32 v[42:43], v[28:29], v[44:45]
	v_pk_add_f32 v[28:29], v[28:29], v[44:45] neg_lo:[0,1] neg_hi:[0,1]
	s_nop 0
	v_pk_mul_f32 v[44:45], v[28:29], v[48:49] op_sel:[1,0] op_sel_hi:[0,0] neg_lo:[1,1] neg_hi:[0,1]
	s_nop 0
	v_pk_fma_f32 v[28:29], v[28:29], v[48:49], v[44:45] op_sel_hi:[1,0,1] neg_lo:[0,1,0] neg_hi:[0,1,0]
	s_waitcnt lgkmcnt(0)
	v_pk_add_f32 v[44:45], v[30:31], v[46:47]
	v_pk_add_f32 v[30:31], v[30:31], v[46:47] neg_lo:[0,1] neg_hi:[0,1]
	s_nop 0
	v_pk_mul_f32 v[46:47], v[30:31], v[50:51] op_sel:[1,0] op_sel_hi:[0,0] neg_lo:[1,1] neg_hi:[0,1]
	v_pk_add_f32 v[50:51], v[32:33], v[24:25]
	v_pk_add_f32 v[24:25], v[32:33], v[24:25] neg_lo:[0,1] neg_hi:[0,1]
	v_pk_fma_f32 v[30:31], v[30:31], v[10:11], v[46:47] op_sel_hi:[1,0,1] neg_lo:[0,1,0] neg_hi:[0,1,0]
	v_pk_mul_f32 v[32:33], v[24:25], v[48:49] op_sel:[1,0] op_sel_hi:[0,0] neg_lo:[1,1] neg_hi:[0,1]
	v_pk_add_f32 v[46:47], v[52:53], v[38:39]
	v_pk_fma_f32 v[24:25], v[24:25], v[48:49], v[32:33] op_sel_hi:[1,0,1]
	v_pk_add_f32 v[32:33], v[34:35], v[42:43]
	v_pk_add_f32 v[34:35], v[34:35], v[42:43] neg_lo:[0,1] neg_hi:[0,1]
	v_pk_add_f32 v[38:39], v[52:53], v[38:39] neg_lo:[0,1] neg_hi:[0,1]
	v_xor_b32_e32 v43, 0x80000000, v34
	v_mov_b32_e32 v42, v35
	v_pk_add_f32 v[34:35], v[36:37], v[44:45]
	v_pk_add_f32 v[36:37], v[36:37], v[44:45] neg_lo:[0,1] neg_hi:[0,1]
	v_mov_b32_e32 v10, v184
	v_pk_mul_f32 v[44:45], v[36:37], v[48:49] op_sel:[1,0] op_sel_hi:[0,0] neg_lo:[1,1] neg_hi:[0,1]
	s_nop 0
	v_pk_fma_f32 v[36:37], v[36:37], v[48:49], v[44:45] op_sel_hi:[1,0,1] neg_lo:[0,1,0] neg_hi:[0,1,0]
	v_pk_add_f32 v[44:45], v[46:47], v[32:33]
	v_pk_add_f32 v[32:33], v[46:47], v[32:33] neg_lo:[0,1] neg_hi:[0,1]
	v_pk_add_f32 v[46:47], v[50:51], v[34:35]
	v_pk_add_f32 v[34:35], v[50:51], v[34:35] neg_lo:[0,1] neg_hi:[0,1]
	s_nop 0
	v_xor_b32_e32 v51, 0x80000000, v34
	v_mov_b32_e32 v50, v35
	v_pk_add_f32 v[34:35], v[44:45], v[46:47]
	v_pk_add_f32 v[44:45], v[44:45], v[46:47] neg_lo:[0,1] neg_hi:[0,1]
	v_pk_add_f32 v[46:47], v[32:33], v[50:51]
	v_pk_add_f32 v[32:33], v[32:33], v[50:51] neg_lo:[0,1] neg_hi:[0,1]
	v_pk_add_f32 v[50:51], v[38:39], v[42:43]
	v_pk_add_f32 v[38:39], v[38:39], v[42:43] neg_lo:[0,1] neg_hi:[0,1]
	v_pk_add_f32 v[42:43], v[24:25], v[36:37]
	v_pk_add_f32 v[24:25], v[24:25], v[36:37] neg_lo:[0,1] neg_hi:[0,1]
	s_nop 0
	v_xor_b32_e32 v37, 0x80000000, v24
	v_mov_b32_e32 v36, v25
	v_pk_add_f32 v[24:25], v[50:51], v[42:43]
	v_pk_add_f32 v[42:43], v[50:51], v[42:43] neg_lo:[0,1] neg_hi:[0,1]
	v_pk_add_f32 v[50:51], v[38:39], v[36:37]
	v_pk_add_f32 v[36:37], v[38:39], v[36:37] neg_lo:[0,1] neg_hi:[0,1]
	v_pk_add_f32 v[38:39], v[16:17], v[40:41]
	v_pk_add_f32 v[16:17], v[16:17], v[40:41] neg_lo:[0,1] neg_hi:[0,1]
	v_pk_add_f32 v[40:41], v[18:19], v[26:27]
	v_pk_add_f32 v[18:19], v[18:19], v[26:27] neg_lo:[0,1] neg_hi:[0,1]
	s_nop 0
	v_pk_mul_f32 v[26:27], v[48:49], v[18:19] op_sel:[0,1] op_sel_hi:[0,0] neg_lo:[1,1] neg_hi:[1,0]
	v_pk_fma_f32 v[18:19], v[48:49], v[18:19], v[26:27] op_sel_hi:[0,1,1]
	v_pk_add_f32 v[26:27], v[20:21], v[28:29]
	v_pk_add_f32 v[20:21], v[20:21], v[28:29] neg_lo:[0,1] neg_hi:[0,1]
	s_nop 0
	v_xor_b32_e32 v29, 0x80000000, v20
	v_mov_b32_e32 v28, v21
	v_pk_add_f32 v[20:21], v[22:23], v[30:31]
	v_pk_add_f32 v[22:23], v[22:23], v[30:31] neg_lo:[0,1] neg_hi:[0,1]
	s_nop 0
	v_pk_mul_f32 v[30:31], v[48:49], v[22:23] op_sel:[0,1] op_sel_hi:[0,0] neg_lo:[1,1] neg_hi:[1,0]
	v_pk_fma_f32 v[22:23], v[48:49], v[22:23], v[30:31] op_sel_hi:[0,1,1] neg_lo:[1,0,0] neg_hi:[1,0,0]
	v_pk_add_f32 v[30:31], v[38:39], v[26:27]
	v_pk_add_f32 v[26:27], v[38:39], v[26:27] neg_lo:[0,1] neg_hi:[0,1]
	v_pk_add_f32 v[38:39], v[40:41], v[20:21]
	v_pk_add_f32 v[20:21], v[40:41], v[20:21] neg_lo:[0,1] neg_hi:[0,1]
	s_nop 0
	v_xor_b32_e32 v41, 0x80000000, v20
	v_mov_b32_e32 v40, v21
	v_pk_add_f32 v[20:21], v[30:31], v[38:39]
	v_pk_add_f32 v[30:31], v[30:31], v[38:39] neg_lo:[0,1] neg_hi:[0,1]
	v_pk_add_f32 v[38:39], v[26:27], v[40:41]
	v_pk_add_f32 v[26:27], v[26:27], v[40:41] neg_lo:[0,1] neg_hi:[0,1]
	v_pk_add_f32 v[40:41], v[16:17], v[28:29]
	v_pk_add_f32 v[16:17], v[16:17], v[28:29] neg_lo:[0,1] neg_hi:[0,1]
	v_pk_add_f32 v[28:29], v[18:19], v[22:23]
	v_pk_add_f32 v[18:19], v[18:19], v[22:23] neg_lo:[0,1] neg_hi:[0,1]
	s_nop 0
	v_xor_b32_e32 v23, 0x80000000, v18
	v_mov_b32_e32 v22, v19
	v_pk_add_f32 v[18:19], v[40:41], v[28:29]
	v_pk_add_f32 v[28:29], v[40:41], v[28:29] neg_lo:[0,1] neg_hi:[0,1]
	v_pk_add_f32 v[40:41], v[16:17], v[22:23]
	v_pk_add_f32 v[16:17], v[16:17], v[22:23] neg_lo:[0,1] neg_hi:[0,1]
	v_add_u32_e32 v22, 0x2000, v14
	v_ashrrev_i32_e32 v23, 31, v22
	v_lshl_add_u64 v[22:23], v[22:23], 3, s[48:49]
	global_store_dwordx2 v[22:23], v[34:35], off
	v_add_u32_e32 v22, 0x2200, v14
	v_ashrrev_i32_e32 v23, 31, v22
	v_lshl_add_u64 v[22:23], v[22:23], 3, s[48:49]
	global_store_dwordx2 v[22:23], v[20:21], off
	v_add_u32_e32 v20, 0x2400, v14
	v_ashrrev_i32_e32 v21, 31, v20
	v_lshl_add_u64 v[20:21], v[20:21], 3, s[48:49]
	global_store_dwordx2 v[20:21], v[24:25], off
	v_add_u32_e32 v20, 0x2600, v14
	v_ashrrev_i32_e32 v21, 31, v20
	v_lshl_add_u64 v[20:21], v[20:21], 3, s[48:49]
	global_store_dwordx2 v[20:21], v[18:19], off
	v_add_u32_e32 v18, 0x2800, v14
	v_ashrrev_i32_e32 v19, 31, v18
	v_lshl_add_u64 v[18:19], v[18:19], 3, s[48:49]
	global_store_dwordx2 v[18:19], v[46:47], off
	v_add_u32_e32 v18, 0x2a00, v14
	v_ashrrev_i32_e32 v19, 31, v18
	v_lshl_add_u64 v[18:19], v[18:19], 3, s[48:49]
	global_store_dwordx2 v[18:19], v[38:39], off
	v_add_u32_e32 v18, 0x2c00, v14
	v_ashrrev_i32_e32 v19, 31, v18
	v_lshl_add_u64 v[18:19], v[18:19], 3, s[48:49]
	global_store_dwordx2 v[18:19], v[50:51], off
	v_add_u32_e32 v18, 0x2e00, v14
	v_ashrrev_i32_e32 v19, 31, v18
	v_lshl_add_u64 v[18:19], v[18:19], 3, s[48:49]
	global_store_dwordx2 v[18:19], v[40:41], off
	v_add_u32_e32 v18, 0x3000, v14
	v_ashrrev_i32_e32 v19, 31, v18
	v_lshl_add_u64 v[18:19], v[18:19], 3, s[48:49]
	global_store_dwordx2 v[18:19], v[44:45], off
	v_add_u32_e32 v18, 0x3200, v14
	v_ashrrev_i32_e32 v19, 31, v18
	v_lshl_add_u64 v[18:19], v[18:19], 3, s[48:49]
	global_store_dwordx2 v[18:19], v[30:31], off
	v_add_u32_e32 v18, 0x3400, v14
	v_ashrrev_i32_e32 v19, 31, v18
	v_lshl_add_u64 v[18:19], v[18:19], 3, s[48:49]
	global_store_dwordx2 v[18:19], v[42:43], off
	v_add_u32_e32 v18, 0x3600, v14
	v_ashrrev_i32_e32 v19, 31, v18
	v_lshl_add_u64 v[18:19], v[18:19], 3, s[48:49]
	global_store_dwordx2 v[18:19], v[28:29], off
	v_add_u32_e32 v18, 0x3800, v14
	v_ashrrev_i32_e32 v19, 31, v18
	v_lshl_add_u64 v[18:19], v[18:19], 3, s[48:49]
	global_store_dwordx2 v[18:19], v[32:33], off
	v_add_u32_e32 v18, 0x3a00, v14
	v_ashrrev_i32_e32 v19, 31, v18
	v_lshl_add_u64 v[18:19], v[18:19], 3, s[48:49]
	global_store_dwordx2 v[18:19], v[26:27], off
	v_add_u32_e32 v18, 0x3c00, v14
	v_add_u32_e32 v14, 0x3e00, v14
	v_ashrrev_i32_e32 v15, 31, v14
	v_ashrrev_i32_e32 v19, 31, v18
	v_lshl_add_u64 v[14:15], v[14:15], 3, s[48:49]
	v_lshl_add_u64 v[18:19], v[18:19], 3, s[48:49]
	global_store_dwordx2 v[14:15], v[16:17], off
	v_mov_b32_e32 v16, v185
	v_mov_b32_e32 v14, v1
	global_store_dwordx2 v[18:19], v[36:37], off
	s_barrier
	s_nop 0
	v_pk_mul_f32 v[36:37], v[16:17], s[66:67] op_sel_hi:[0,1] neg_lo:[1,0]
	s_mov_b64 s[66:67], vcc
	v_ashrrev_i32_e32 v15, 31, v14
	v_lshl_add_u64 v[18:19], v[14:15], 2, s[66:67]
	v_add_co_u32_e32 v28, vcc, s85, v18
	v_pk_mul_f32 v[52:53], v[16:17], s[60:61] op_sel_hi:[0,1] neg_lo:[1,0]
	s_nop 0
	v_addc_co_u32_e32 v29, vcc, 0, v19, vcc
	v_add_co_u32_e32 v20, vcc, s84, v18
	s_movk_i32 s61, 0x3000
	s_nop 0
	v_addc_co_u32_e32 v21, vcc, 0, v19, vcc
	v_add_co_u32_e32 v48, vcc, s61, v18
	v_pk_mul_f32 v[54:55], v[16:17], s[94:95] op_sel_hi:[0,1] neg_lo:[1,0]
	s_nop 0
	v_addc_co_u32_e32 v49, vcc, 0, v19, vcc
	v_add_co_u32_e32 v22, vcc, s45, v18
	v_pk_mul_f32 v[82:83], v[16:17], s[68:69] op_sel_hi:[0,1] neg_lo:[1,0]
	s_nop 0
	v_addc_co_u32_e32 v23, vcc, 0, v19, vcc
	v_add_co_u32_e32 v58, vcc, s86, v18
	s_mov_b32 s68, 0x3f7ec46d
	s_nop 0
	v_addc_co_u32_e32 v59, vcc, 0, v19, vcc
	v_add_co_u32_e32 v60, vcc, s88, v18
	v_pk_mul_f32 v[32:33], v[16:17], s[78:79] op_sel_hi:[0,1] neg_lo:[1,0]
	s_nop 0
	v_addc_co_u32_e32 v61, vcc, 0, v19, vcc
	v_add_co_u32_e32 v66, vcc, s90, v18
	v_pk_mul_f32 v[40:41], v[16:17], s[80:81] op_sel_hi:[0,1] neg_lo:[1,0]
	s_nop 0
	v_addc_co_u32_e32 v67, vcc, 0, v19, vcc
	v_add_co_u32_e32 v68, vcc, s39, v18
	s_mov_b32 s39, 0x9000
	s_nop 0
	v_addc_co_u32_e32 v69, vcc, 0, v19, vcc
	v_add_co_u32_e32 v24, vcc, s39, v18
	s_mov_b32 s39, 0xb000
	s_nop 0
	v_addc_co_u32_e32 v25, vcc, 0, v19, vcc
	v_add_co_u32_e32 v26, vcc, s91, v18
	s_mov_b32 s80, 0x3f54db31
	s_nop 0
	v_addc_co_u32_e32 v27, vcc, 0, v19, vcc
	v_add_co_u32_e32 v34, vcc, s39, v18
	s_mov_b32 s39, 0xc000
	s_nop 0
	v_addc_co_u32_e32 v35, vcc, 0, v19, vcc
	v_add_co_u32_e32 v38, vcc, s39, v18
	s_mov_b32 s39, 0xd000
	s_nop 0
	v_addc_co_u32_e32 v39, vcc, 0, v19, vcc
	v_add_co_u32_e32 v46, vcc, s39, v18
	s_mov_b32 s39, 0xe000
	s_nop 0
	v_addc_co_u32_e32 v47, vcc, 0, v19, vcc
	v_add_co_u32_e32 v50, vcc, s39, v18
	s_mov_b32 s39, 0xf000
	s_nop 0
	v_addc_co_u32_e32 v51, vcc, 0, v19, vcc
	v_add_co_u32_e32 v70, vcc, s39, v18
	s_mov_b32 s69, 0xbdc8bd36
	s_nop 0
	v_addc_co_u32_e32 v71, vcc, 0, v19, vcc
	global_load_dword v90, v[68:69], off
	global_load_dword v92, v[68:69], off offset:2048
	global_load_dword v94, v[26:27], off offset:-4096
	global_load_dword v96, v[24:25], off offset:2048
	global_load_dword v98, v[26:27], off
	global_load_dword v100, v[26:27], off offset:2048
	global_load_dword v102, v[38:39], off offset:-4096
	global_load_dword v104, v[34:35], off offset:2048
	global_load_dword v106, v[38:39], off
	global_load_dword v108, v[38:39], off offset:2048
	global_load_dword v110, v[50:51], off offset:-4096
	global_load_dword v112, v[46:47], off offset:2048
	global_load_dword v114, v[50:51], off
	global_load_dword v116, v[50:51], off offset:2048
	global_load_dword v118, v[70:71], off
	global_load_dword v56, v[20:21], off
	s_nop 0
	global_load_dword v50, v[20:21], off offset:2048
	global_load_dword v120, v[70:71], off offset:2048
	global_load_dword v46, v[22:23], off offset:-4096
	global_load_dword v38, v[22:23], off
	global_load_dword v74, v[20:21], off offset:-4096
	global_load_dword v34, v[22:23], off offset:2048
	global_load_dword v26, v[60:61], off offset:-4096
	global_load_dword v24, v[60:61], off
	s_nop 0
	global_load_dword v22, v[60:61], off offset:2048
	global_load_dword v20, v[68:69], off offset:-4096
	s_nop 0
	global_load_dword v68, v[18:19], off
	global_load_dword v76, v[18:19], off offset:2048
	global_load_dword v72, v[28:29], off offset:2048
	s_nop 0
	global_load_dword v48, v[48:49], off offset:2048
	s_nop 0
	global_load_dword v28, v[58:59], off offset:2048
	global_load_dword v18, v[66:67], off offset:2048
	s_mov_b32 s88, 0x3e47c5c2
	v_pk_fma_f32 v[58:59], v[10:11], s[74:75], v[54:55] op_sel_hi:[0,1,1]
	s_mov_b32 s74, 0x3f226799
	s_mov_b32 s81, 0xbf0e39da
	v_pk_mul_f32 v[42:43], v[16:17], s[52:53] op_sel_hi:[0,1] neg_lo:[1,0]
	v_pk_mul_f32 v[64:65], v[16:17], s[62:63] op_sel_hi:[0,1] neg_lo:[1,0]
	s_mov_b32 s89, 0xbf7b14be
	v_pk_fma_f32 v[124:125], v[10:11], s[68:69], v[32:33] op_sel_hi:[0,1,1]
	s_mov_b32 s75, 0xbf45e403
	s_mov_b32 s52, 0x3f3504f3
	v_pk_mul_f32 v[32:33], v[16:17], s[30:31] op_sel_hi:[0,1] neg_lo:[1,0]
	s_mov_b32 s30, 0x3dc8bd36
	v_pk_mul_f32 v[62:63], v[16:17], s[56:57] op_sel_hi:[0,1] neg_lo:[1,0]
	v_pk_fma_f32 v[60:61], v[10:11], s[80:81], v[52:53] op_sel_hi:[0,1,1]
	s_mov_b32 s53, 0xbf3504f3
	v_pk_fma_f32 v[52:53], v[10:11], s[74:75], v[64:65] op_sel_hi:[0,1,1]
	s_mov_b32 s31, 0xbf7ec46d
	v_pk_fma_f32 v[64:65], v[10:11], s[88:89], v[32:33] op_sel_hi:[0,1,1]
	v_pk_mul_f32 v[32:33], v[16:17], s[34:35] op_sel_hi:[0,1] neg_lo:[1,0]
	s_mov_b32 s78, 0x3f61c598
	v_pk_fma_f32 v[54:55], v[10:11], s[52:53], v[62:63] op_sel_hi:[0,1,1]
	v_pk_fma_f32 v[62:63], v[10:11], s[30:31], v[32:33] op_sel_hi:[0,1,1]
	v_pk_mul_f32 v[32:33], v[16:17], s[36:37] op_sel_hi:[0,1] neg_lo:[1,0]
	s_mov_b32 s79, 0xbef15aea
	v_pk_mul_f32 v[44:45], v[16:17], s[50:51] op_sel_hi:[0,1] neg_lo:[1,0]
	v_pk_fma_f32 v[32:33], v[10:11], s[76:77], v[32:33] op_sel_hi:[0,1,1]
	s_mov_b32 s94, 0x3f6c835e
	v_pk_fma_f32 v[66:67], v[10:11], s[78:79], v[44:45] op_sel_hi:[0,1,1]
	v_pk_fma_f32 v[44:45], v[10:11], s[82:83], v[82:83] op_sel_hi:[0,1,1]
	s_mov_b32 s82, 0x3ef15aea
	s_mov_b32 s95, 0xbec3ef15
	v_pk_mul_f32 v[84:85], v[16:17], s[70:71] op_sel_hi:[0,1] neg_lo:[1,0]
	s_mov_b32 s83, 0xbf61c598
	v_pk_mul_f32 v[30:31], v[16:17], s[40:41] op_sel_hi:[0,1] neg_lo:[1,0]
	s_mov_b32 s84, 0x3ec3ef15
	s_mov_b32 s40, 0x3f74fa0b
	v_pk_fma_f32 v[70:71], v[10:11], s[94:95], v[42:43] op_sel_hi:[0,1,1]
	v_pk_fma_f32 v[42:43], v[10:11], s[82:83], v[84:85] op_sel_hi:[0,1,1]
	s_mov_b32 s85, 0xbf6c835e
	s_mov_b32 s41, 0xbe94a031
	v_pk_mul_f32 v[86:87], v[16:17], s[58:59] op_sel_hi:[0,1] neg_lo:[1,0]
	s_mov_b32 s86, 0x3e94a031
	v_pk_fma_f32 v[78:79], v[10:11], s[40:41], v[40:41] op_sel_hi:[0,1,1]
	v_pk_fma_f32 v[40:41], v[10:11], s[84:85], v[86:87] op_sel_hi:[0,1,1]
	s_mov_b32 s87, 0xbf74fa0b
	v_pk_mul_f32 v[88:89], v[16:17], s[64:65] op_sel_hi:[0,1] neg_lo:[1,0]
	v_pk_fma_f32 v[122:123], v[10:11], s[46:47], v[30:31] op_sel_hi:[0,1,1]
	v_pk_fma_f32 v[30:31], v[10:11], s[86:87], v[88:89] op_sel_hi:[0,1,1]
	s_waitcnt vmcnt(31)
	v_pk_mul_f32 v[82:83], v[32:33], v[90:91] op_sel_hi:[1,0]
	v_pk_mul_f32 v[32:33], v[16:17], s[2:3] op_sel_hi:[0,1] neg_lo:[1,0]
	v_pk_fma_f32 v[32:33], v[10:11], s[0:1], v[32:33] op_sel_hi:[0,1,1]
	s_waitcnt vmcnt(30)
	v_pk_mul_f32 v[84:85], v[32:33], v[92:93] op_sel_hi:[1,0]
	v_pk_mul_f32 v[32:33], v[16:17], s[6:7] op_sel_hi:[0,1] neg_lo:[1,0]
	v_pk_fma_f32 v[32:33], v[10:11], s[4:5], v[32:33] op_sel_hi:[0,1,1]
	s_waitcnt vmcnt(29)
	v_pk_mul_f32 v[86:87], v[32:33], v[94:95] op_sel_hi:[1,0]
	v_pk_mul_f32 v[32:33], v[16:17], s[10:11] op_sel_hi:[0,1] neg_lo:[1,0]
	v_pk_fma_f32 v[32:33], v[10:11], s[8:9], v[32:33] op_sel_hi:[0,1,1]
	s_waitcnt vmcnt(28)
	v_pk_mul_f32 v[88:89], v[32:33], v[96:97] op_sel_hi:[1,0]
	v_pk_mul_f32 v[32:33], v[16:17], s[16:17] op_sel_hi:[0,1] neg_lo:[1,0]
	v_pk_fma_f32 v[32:33], v[10:11], s[12:13], v[32:33] op_sel_hi:[0,1,1]
	s_waitcnt vmcnt(27)
	v_pk_mul_f32 v[90:91], v[32:33], v[98:99] op_sel_hi:[1,0]
	v_pk_mul_f32 v[32:33], v[16:17], s[20:21] op_sel_hi:[0,1] neg_lo:[1,0]
	v_pk_fma_f32 v[32:33], v[10:11], s[18:19], v[32:33] op_sel_hi:[0,1,1]
	s_waitcnt vmcnt(26)
	v_pk_mul_f32 v[92:93], v[32:33], v[100:101] op_sel_hi:[1,0]
	v_pk_mul_f32 v[32:33], v[16:17], s[24:25] op_sel_hi:[0,1] neg_lo:[1,0]
	v_pk_fma_f32 v[32:33], v[10:11], s[22:23], v[32:33] op_sel_hi:[0,1,1]
	s_waitcnt vmcnt(25)
	v_pk_mul_f32 v[94:95], v[32:33], v[102:103] op_sel_hi:[1,0]
	v_pk_mul_f32 v[32:33], v[16:17], s[28:29] op_sel_hi:[0,1] neg_lo:[1,0]
	v_pk_fma_f32 v[32:33], v[10:11], s[26:27], v[32:33] op_sel_hi:[0,1,1]
	s_waitcnt vmcnt(24)
	v_pk_mul_f32 v[96:97], v[32:33], v[104:105] op_sel_hi:[1,0]
	v_pk_mul_f32 v[32:33], v[16:17], s[52:53] op_sel_hi:[0,0] neg_lo:[1,0]
	v_pk_fma_f32 v[32:33], v[10:11], s[38:39], v[32:33] op_sel_hi:[0,0,1] neg_lo:[0,0,1] neg_hi:[0,0,1]
	s_waitcnt vmcnt(23)
	v_pk_mul_f32 v[98:99], v[32:33], v[106:107] op_sel_hi:[1,0]
	v_pk_mul_f32 v[32:33], v[16:17], s[26:27] op_sel_hi:[0,1] neg_lo:[1,0]
	v_pk_fma_f32 v[32:33], v[10:11], s[28:29], v[32:33] op_sel_hi:[0,1,1]
	s_waitcnt vmcnt(22)
	v_pk_mul_f32 v[100:101], v[32:33], v[108:109] op_sel_hi:[1,0]
	v_pk_mul_f32 v[32:33], v[16:17], s[22:23] op_sel_hi:[0,1] neg_lo:[1,0]
	v_pk_fma_f32 v[32:33], v[10:11], s[24:25], v[32:33] op_sel_hi:[0,1,1]
	s_waitcnt vmcnt(21)
	v_pk_mul_f32 v[102:103], v[32:33], v[110:111] op_sel_hi:[1,0]
	v_pk_mul_f32 v[32:33], v[16:17], s[18:19] op_sel_hi:[0,1] neg_lo:[1,0]
	v_pk_fma_f32 v[32:33], v[10:11], s[20:21], v[32:33] op_sel_hi:[0,1,1]
	s_waitcnt vmcnt(20)
	v_pk_mul_f32 v[104:105], v[32:33], v[112:113] op_sel_hi:[1,0]
	v_pk_mul_f32 v[32:33], v[16:17], s[12:13] op_sel_hi:[0,1] neg_lo:[1,0]
	v_pk_fma_f32 v[32:33], v[10:11], s[16:17], v[32:33] op_sel_hi:[0,1,1]
	s_waitcnt vmcnt(19)
	v_pk_mul_f32 v[106:107], v[32:33], v[114:115] op_sel_hi:[1,0]
	v_pk_mul_f32 v[32:33], v[16:17], s[8:9] op_sel_hi:[0,1] neg_lo:[1,0]
	v_pk_fma_f32 v[32:33], v[10:11], s[10:11], v[32:33] op_sel_hi:[0,1,1]
	s_mov_b32 s70, 0x3f7b14be
	s_waitcnt vmcnt(18)
	v_pk_mul_f32 v[108:109], v[32:33], v[116:117] op_sel_hi:[1,0]
	v_pk_mul_f32 v[32:33], v[16:17], s[4:5] op_sel_hi:[0,1] neg_lo:[1,0]
	v_pk_mul_f32 v[16:17], v[16:17], s[0:1] op_sel_hi:[0,1] neg_lo:[1,0]
	s_mov_b32 s71, 0xbe47c5c2
	v_pk_fma_f32 v[16:17], v[10:11], s[2:3], v[16:17] op_sel_hi:[0,1,1]
	v_pk_fma_f32 v[80:81], v[10:11], s[70:71], v[36:37] op_sel_hi:[0,1,1]
	v_pk_fma_f32 v[32:33], v[10:11], s[6:7], v[32:33] op_sel_hi:[0,1,1]
	s_waitcnt vmcnt(14)
	v_pk_mul_f32 v[112:113], v[16:17], v[120:121] op_sel_hi:[1,0]
	s_waitcnt vmcnt(5)
	v_pk_fma_f32 v[126:127], v[68:69], v[122:123], v[82:83] op_sel_hi:[0,1,1]
	v_pk_fma_f32 v[68:69], v[68:69], v[122:123], v[82:83] op_sel_hi:[0,1,1] neg_lo:[0,0,1] neg_hi:[0,0,1]
	s_waitcnt vmcnt(4)
	v_pk_fma_f32 v[82:83], v[124:125], v[76:77], v[84:85] op_sel_hi:[1,0,1]
	v_pk_fma_f32 v[76:77], v[124:125], v[76:77], v[84:85] op_sel_hi:[1,0,1] neg_lo:[0,0,1] neg_hi:[0,0,1]
	v_pk_mul_f32 v[110:111], v[32:33], v[118:119] op_sel_hi:[1,0]
	v_mov_b32_e32 v114, v165
	v_mov_b32_e32 v32, v166
	v_mov_b32_e32 v116, v167
	v_mov_b32_e32 v10, v168
	v_mov_b32_e32 v118, v169
	v_mov_b32_e32 v36, v170
	v_mov_b32_e32 v120, v171
	v_pk_mul_f32 v[84:85], v[76:77], v[120:121] op_sel:[1,0] op_sel_hi:[0,0] neg_lo:[1,1] neg_hi:[0,1]
	s_nop 0
	v_pk_fma_f32 v[76:77], v[76:77], v[114:115], v[84:85] op_sel_hi:[1,0,1]
	v_pk_fma_f32 v[84:85], v[80:81], v[74:75], v[86:87] op_sel_hi:[1,0,1]
	v_pk_fma_f32 v[74:75], v[80:81], v[74:75], v[86:87] op_sel_hi:[1,0,1] neg_lo:[0,0,1] neg_hi:[0,0,1]
	s_nop 0
	v_pk_mul_f32 v[80:81], v[74:75], v[36:37] op_sel:[1,0] op_sel_hi:[0,0] neg_lo:[1,1] neg_hi:[0,1]
	s_nop 0
	v_pk_fma_f32 v[74:75], v[74:75], v[32:33], v[80:81] op_sel_hi:[1,0,1]
	s_waitcnt vmcnt(3)
	v_pk_fma_f32 v[80:81], v[78:79], v[72:73], v[88:89] op_sel_hi:[1,0,1]
	v_pk_fma_f32 v[72:73], v[78:79], v[72:73], v[88:89] op_sel_hi:[1,0,1] neg_lo:[0,0,1] neg_hi:[0,0,1]
	s_nop 0
	v_pk_mul_f32 v[78:79], v[72:73], v[118:119] op_sel:[1,0] op_sel_hi:[0,0] neg_lo:[1,1] neg_hi:[0,1]
	s_nop 0
	v_pk_fma_f32 v[72:73], v[72:73], v[116:117], v[78:79] op_sel_hi:[1,0,1]
	v_pk_fma_f32 v[78:79], v[70:71], v[56:57], v[90:91] op_sel_hi:[1,0,1]
	v_pk_fma_f32 v[56:57], v[70:71], v[56:57], v[90:91] op_sel_hi:[1,0,1] neg_lo:[0,0,1] neg_hi:[0,0,1]
	s_nop 0
	v_pk_mul_f32 v[70:71], v[56:57], v[10:11] op_sel:[1,0] op_sel_hi:[0,0] neg_lo:[1,1] neg_hi:[0,1]
	s_nop 0
	v_pk_fma_f32 v[56:57], v[56:57], v[10:11], v[70:71] op_sel_hi:[1,0,1]
	v_pk_fma_f32 v[70:71], v[66:67], v[50:51], v[92:93] op_sel_hi:[1,0,1]
	v_pk_fma_f32 v[50:51], v[66:67], v[50:51], v[92:93] op_sel_hi:[1,0,1] neg_lo:[0,0,1] neg_hi:[0,0,1]
	s_nop 0
	v_pk_mul_f32 v[66:67], v[50:51], v[118:119] op_sel_hi:[1,0]
	v_xor_b32_e32 v86, 0x80000000, v51
	v_mov_b32_e32 v87, v50
	v_pk_fma_f32 v[50:51], v[60:61], v[46:47], v[94:95] op_sel_hi:[1,0,1]
	v_pk_fma_f32 v[46:47], v[60:61], v[46:47], v[94:95] op_sel_hi:[1,0,1] neg_lo:[0,0,1] neg_hi:[0,0,1]
	v_pk_fma_f32 v[66:67], v[86:87], v[116:117], v[66:67] op_sel_hi:[1,0,1] neg_lo:[0,1,0] neg_hi:[0,1,0]
	v_pk_mul_f32 v[60:61], v[46:47], v[36:37] op_sel_hi:[1,0]
	v_xor_b32_e32 v86, 0x80000000, v47
	v_mov_b32_e32 v87, v46
	s_waitcnt vmcnt(2)
	v_pk_fma_f32 v[46:47], v[58:59], v[48:49], v[96:97] op_sel_hi:[1,0,1]
	v_pk_fma_f32 v[48:49], v[58:59], v[48:49], v[96:97] op_sel_hi:[1,0,1] neg_lo:[0,0,1] neg_hi:[0,0,1]
	v_pk_fma_f32 v[60:61], v[86:87], v[32:33], v[60:61] op_sel_hi:[1,0,1] neg_lo:[0,1,0] neg_hi:[0,1,0]
	v_pk_mul_f32 v[58:59], v[48:49], v[120:121] op_sel_hi:[1,0]
	s_nop 0
	v_pk_fma_f32 v[48:49], v[48:49], v[114:115], v[58:59] op_sel:[1,0,0] op_sel_hi:[0,0,1] neg_lo:[1,1,0] neg_hi:[0,1,0]
	v_pk_fma_f32 v[58:59], v[54:55], v[38:39], v[98:99] op_sel_hi:[1,0,1]
	v_pk_fma_f32 v[38:39], v[54:55], v[38:39], v[98:99] op_sel_hi:[1,0,1] neg_lo:[0,0,1] neg_hi:[0,0,1]
	s_nop 0
	v_xor_b32_e32 v55, 0x80000000, v38
	v_mov_b32_e32 v54, v39
	v_pk_fma_f32 v[38:39], v[52:53], v[34:35], v[100:101] op_sel_hi:[1,0,1]
	v_pk_fma_f32 v[34:35], v[52:53], v[34:35], v[100:101] op_sel_hi:[1,0,1] neg_lo:[0,0,1] neg_hi:[0,0,1]
	s_nop 0
	v_pk_mul_f32 v[52:53], v[34:35], v[120:121] op_sel_hi:[1,0] neg_lo:[0,1] neg_hi:[0,1]
	v_xor_b32_e32 v86, 0x80000000, v35
	v_mov_b32_e32 v87, v34
	v_pk_fma_f32 v[34:35], v[44:45], v[26:27], v[102:103] op_sel_hi:[1,0,1]
	v_pk_fma_f32 v[26:27], v[44:45], v[26:27], v[102:103] op_sel_hi:[1,0,1] neg_lo:[0,0,1] neg_hi:[0,0,1]
	v_pk_fma_f32 v[52:53], v[86:87], v[114:115], v[52:53] op_sel_hi:[1,0,1] neg_lo:[0,1,0] neg_hi:[0,1,0]
	v_pk_mul_f32 v[44:45], v[26:27], v[36:37] op_sel_hi:[1,0] neg_lo:[0,1] neg_hi:[0,1]
	v_xor_b32_e32 v86, 0x80000000, v27
	v_mov_b32_e32 v87, v26
	s_waitcnt vmcnt(1)
	v_pk_fma_f32 v[26:27], v[42:43], v[28:29], v[104:105] op_sel_hi:[1,0,1]
	v_pk_fma_f32 v[28:29], v[42:43], v[28:29], v[104:105] op_sel_hi:[1,0,1] neg_lo:[0,0,1] neg_hi:[0,0,1]
	v_pk_fma_f32 v[86:87], v[86:87], v[32:33], v[44:45] op_sel_hi:[1,0,1] neg_lo:[0,1,0] neg_hi:[0,1,0]
	v_pk_mul_f32 v[42:43], v[28:29], v[118:119] op_sel_hi:[1,0] neg_lo:[0,1] neg_hi:[0,1]
	v_xor_b32_e32 v44, 0x80000000, v29
	v_mov_b32_e32 v45, v28
	v_pk_fma_f32 v[28:29], v[40:41], v[24:25], v[106:107] op_sel_hi:[1,0,1]
	v_pk_fma_f32 v[24:25], v[40:41], v[24:25], v[106:107] op_sel_hi:[1,0,1] neg_lo:[0,0,1] neg_hi:[0,0,1]
	v_pk_fma_f32 v[42:43], v[44:45], v[116:117], v[42:43] op_sel_hi:[1,0,1] neg_lo:[0,1,0] neg_hi:[0,1,0]
	v_pk_mul_f32 v[40:41], v[24:25], v[10:11] op_sel:[1,0] op_sel_hi:[0,0] neg_lo:[1,1] neg_hi:[0,1]
	v_pk_add_f32 v[44:45], v[126:127], v[58:59] neg_lo:[0,1] neg_hi:[0,1]
	v_pk_fma_f32 v[88:89], v[24:25], v[10:11], v[40:41] op_sel_hi:[1,0,1] neg_lo:[0,1,0] neg_hi:[0,1,0]
	v_pk_fma_f32 v[24:25], v[30:31], v[22:23], v[108:109] op_sel_hi:[1,0,1]
	v_pk_fma_f32 v[22:23], v[30:31], v[22:23], v[108:109] op_sel_hi:[1,0,1] neg_lo:[0,0,1] neg_hi:[0,0,1]
	s_nop 0
	v_pk_mul_f32 v[30:31], v[22:23], v[118:119] op_sel:[1,0] op_sel_hi:[0,0] neg_lo:[1,1] neg_hi:[0,1]
	s_nop 0
	v_pk_fma_f32 v[90:91], v[22:23], v[116:117], v[30:31] op_sel_hi:[1,0,1] neg_lo:[0,1,0] neg_hi:[0,1,0]
	v_pk_fma_f32 v[22:23], v[64:65], v[20:21], v[110:111] op_sel_hi:[1,0,1]
	v_pk_fma_f32 v[20:21], v[64:65], v[20:21], v[110:111] op_sel_hi:[1,0,1] neg_lo:[0,0,1] neg_hi:[0,0,1]
	s_nop 0
	v_pk_mul_f32 v[30:31], v[20:21], v[36:37] op_sel:[1,0] op_sel_hi:[0,0] neg_lo:[1,1] neg_hi:[0,1]
	s_nop 0
	v_pk_fma_f32 v[64:65], v[20:21], v[32:33], v[30:31] op_sel_hi:[1,0,1] neg_lo:[0,1,0] neg_hi:[0,1,0]
	s_waitcnt vmcnt(0)
	v_pk_fma_f32 v[20:21], v[62:63], v[18:19], v[112:113] op_sel_hi:[1,0,1]
	v_pk_fma_f32 v[18:19], v[62:63], v[18:19], v[112:113] op_sel_hi:[1,0,1] neg_lo:[0,0,1] neg_hi:[0,0,1]
	s_nop 0
	v_pk_mul_f32 v[30:31], v[18:19], v[120:121] op_sel:[1,0] op_sel_hi:[0,0] neg_lo:[1,1] neg_hi:[0,1]
	s_nop 0
	v_pk_fma_f32 v[62:63], v[18:19], v[114:115], v[30:31] op_sel_hi:[1,0,1] neg_lo:[0,1,0] neg_hi:[0,1,0]
	v_pk_add_f32 v[30:31], v[82:83], v[38:39]
	v_pk_add_f32 v[38:39], v[82:83], v[38:39] neg_lo:[0,1] neg_hi:[0,1]
	v_pk_add_f32 v[18:19], v[126:127], v[58:59]
	v_pk_mul_f32 v[40:41], v[38:39], v[36:37] op_sel:[1,0] op_sel_hi:[0,0] neg_lo:[1,1] neg_hi:[0,1]
	s_nop 0
	v_pk_fma_f32 v[38:39], v[38:39], v[32:33], v[40:41] op_sel_hi:[1,0,1]
	v_pk_add_f32 v[40:41], v[84:85], v[34:35]
	v_pk_add_f32 v[34:35], v[84:85], v[34:35] neg_lo:[0,1] neg_hi:[0,1]
	s_nop 0
	v_pk_mul_f32 v[58:59], v[34:35], v[10:11] op_sel:[1,0] op_sel_hi:[0,0] neg_lo:[1,1] neg_hi:[0,1]
	s_nop 0
	v_pk_fma_f32 v[34:35], v[34:35], v[10:11], v[58:59] op_sel_hi:[1,0,1]
	v_pk_add_f32 v[58:59], v[80:81], v[26:27]
	v_pk_add_f32 v[26:27], v[80:81], v[26:27] neg_lo:[0,1] neg_hi:[0,1]
	s_nop 0
	v_pk_mul_f32 v[80:81], v[26:27], v[36:37] op_sel_hi:[1,0]
	v_xor_b32_e32 v82, 0x80000000, v27
	v_mov_b32_e32 v83, v26
	v_pk_add_f32 v[26:27], v[78:79], v[28:29]
	v_pk_add_f32 v[28:29], v[78:79], v[28:29] neg_lo:[0,1] neg_hi:[0,1]
	v_pk_fma_f32 v[80:81], v[82:83], v[32:33], v[80:81] op_sel_hi:[1,0,1] neg_lo:[0,1,0] neg_hi:[0,1,0]
	v_xor_b32_e32 v79, 0x80000000, v28
	v_mov_b32_e32 v78, v29
	v_pk_add_f32 v[28:29], v[70:71], v[24:25]
	v_pk_add_f32 v[24:25], v[70:71], v[24:25] neg_lo:[0,1] neg_hi:[0,1]
	s_nop 0
	v_pk_mul_f32 v[70:71], v[24:25], v[36:37] op_sel_hi:[1,0] neg_lo:[0,1] neg_hi:[0,1]
	s_nop 0
	v_pk_fma_f32 v[24:25], v[24:25], v[32:33], v[70:71] op_sel:[1,0,0] op_sel_hi:[0,0,1] neg_lo:[1,1,0] neg_hi:[0,1,0]
	v_pk_add_f32 v[70:71], v[50:51], v[22:23]
	v_pk_add_f32 v[22:23], v[50:51], v[22:23] neg_lo:[0,1] neg_hi:[0,1]
	s_nop 0
	v_pk_mul_f32 v[50:51], v[22:23], v[10:11] op_sel:[1,0] op_sel_hi:[0,0] neg_lo:[1,1] neg_hi:[0,1]
	s_nop 0
	v_pk_fma_f32 v[50:51], v[22:23], v[10:11], v[50:51] op_sel_hi:[1,0,1] neg_lo:[0,1,0] neg_hi:[0,1,0]
	v_pk_add_f32 v[22:23], v[46:47], v[20:21]
	v_pk_add_f32 v[20:21], v[46:47], v[20:21] neg_lo:[0,1] neg_hi:[0,1]
	s_nop 0
	v_pk_mul_f32 v[46:47], v[20:21], v[36:37] op_sel:[1,0] op_sel_hi:[0,0] neg_lo:[1,1] neg_hi:[0,1]
	s_nop 0
	v_pk_fma_f32 v[20:21], v[20:21], v[32:33], v[46:47] op_sel_hi:[1,0,1] neg_lo:[0,1,0] neg_hi:[0,1,0]
	v_pk_add_f32 v[46:47], v[18:19], v[26:27]
	v_pk_add_f32 v[18:19], v[18:19], v[26:27] neg_lo:[0,1] neg_hi:[0,1]
	v_pk_add_f32 v[26:27], v[30:31], v[28:29]
	v_pk_add_f32 v[28:29], v[30:31], v[28:29] neg_lo:[0,1] neg_hi:[0,1]
	s_nop 0
	v_pk_mul_f32 v[30:31], v[28:29], v[10:11] op_sel:[1,0] op_sel_hi:[0,0] neg_lo:[1,1] neg_hi:[0,1]
	s_nop 0
	v_pk_fma_f32 v[28:29], v[28:29], v[10:11], v[30:31] op_sel_hi:[1,0,1]
	v_pk_add_f32 v[30:31], v[40:41], v[70:71]
	v_pk_add_f32 v[40:41], v[40:41], v[70:71] neg_lo:[0,1] neg_hi:[0,1]
	v_pk_add_f32 v[82:83], v[46:47], v[30:31] neg_lo:[0,1] neg_hi:[0,1]
	v_xor_b32_e32 v71, 0x80000000, v40
	v_mov_b32_e32 v70, v41
	v_pk_add_f32 v[40:41], v[58:59], v[22:23]
	v_pk_add_f32 v[22:23], v[58:59], v[22:23] neg_lo:[0,1] neg_hi:[0,1]
	s_nop 0
	v_pk_mul_f32 v[58:59], v[22:23], v[10:11] op_sel:[1,0] op_sel_hi:[0,0] neg_lo:[1,1] neg_hi:[0,1]
	s_nop 0
	v_pk_fma_f32 v[58:59], v[22:23], v[10:11], v[58:59] op_sel_hi:[1,0,1] neg_lo:[0,1,0] neg_hi:[0,1,0]
	v_pk_add_f32 v[22:23], v[46:47], v[30:31]
	v_pk_add_f32 v[30:31], v[26:27], v[40:41]
	v_pk_add_f32 v[26:27], v[26:27], v[40:41] neg_lo:[0,1] neg_hi:[0,1]
	v_pk_add_f32 v[84:85], v[22:23], v[30:31]
	v_pk_add_f32 v[30:31], v[22:23], v[30:31] neg_lo:[0,1] neg_hi:[0,1]
	v_pk_add_f32 v[46:47], v[82:83], v[26:27] op_sel:[0,1] op_sel_hi:[1,0] neg_hi:[0,1]
	v_pk_add_f32 v[22:23], v[82:83], v[26:27] op_sel:[0,1] op_sel_hi:[1,0] neg_lo:[0,1]
	v_pk_add_f32 v[40:41], v[28:29], v[58:59]
	v_pk_add_f32 v[28:29], v[28:29], v[58:59] neg_lo:[0,1] neg_hi:[0,1]
	v_pk_add_f32 v[26:27], v[18:19], v[70:71]
	v_pk_add_f32 v[18:19], v[18:19], v[70:71] neg_lo:[0,1] neg_hi:[0,1]
	v_pk_add_f32 v[70:71], v[26:27], v[40:41]
	v_pk_add_f32 v[26:27], v[26:27], v[40:41] neg_lo:[0,1] neg_hi:[0,1]
	v_pk_add_f32 v[40:41], v[18:19], v[28:29] op_sel:[0,1] op_sel_hi:[1,0] neg_hi:[0,1]
	v_pk_add_f32 v[18:19], v[18:19], v[28:29] op_sel:[0,1] op_sel_hi:[1,0] neg_lo:[0,1]
	v_pk_add_f32 v[58:59], v[38:39], v[24:25]
	v_pk_add_f32 v[24:25], v[38:39], v[24:25] neg_lo:[0,1] neg_hi:[0,1]
	v_pk_add_f32 v[28:29], v[44:45], v[78:79]
	v_pk_mul_f32 v[38:39], v[10:11], v[24:25] op_sel:[0,1] op_sel_hi:[0,0] neg_lo:[1,1] neg_hi:[1,0]
	v_pk_fma_f32 v[38:39], v[10:11], v[24:25], v[38:39] op_sel_hi:[0,1,1]
	v_pk_add_f32 v[24:25], v[34:35], v[50:51]
	v_pk_add_f32 v[34:35], v[34:35], v[50:51] neg_lo:[0,1] neg_hi:[0,1]
	v_pk_add_f32 v[44:45], v[44:45], v[78:79] neg_lo:[0,1] neg_hi:[0,1]
	v_xor_b32_e32 v79, 0x80000000, v34
	v_mov_b32_e32 v78, v35
	v_pk_add_f32 v[34:35], v[80:81], v[20:21]
	v_pk_add_f32 v[20:21], v[80:81], v[20:21] neg_lo:[0,1] neg_hi:[0,1]
	s_nop 0
	v_pk_mul_f32 v[50:51], v[10:11], v[20:21] op_sel:[0,1] op_sel_hi:[0,0] neg_lo:[1,1] neg_hi:[1,0]
	v_pk_fma_f32 v[20:21], v[10:11], v[20:21], v[50:51] op_sel_hi:[0,1,1] neg_lo:[1,0,0] neg_hi:[1,0,0]
	v_pk_add_f32 v[50:51], v[28:29], v[24:25]
	v_pk_add_f32 v[24:25], v[28:29], v[24:25] neg_lo:[0,1] neg_hi:[0,1]
	v_pk_add_f32 v[28:29], v[58:59], v[34:35]
	v_pk_add_f32 v[34:35], v[58:59], v[34:35] neg_lo:[0,1] neg_hi:[0,1]
	v_pk_add_f32 v[80:81], v[50:51], v[28:29]
	v_xor_b32_e32 v59, 0x80000000, v34
	v_mov_b32_e32 v58, v35
	v_pk_add_f32 v[34:35], v[50:51], v[28:29] neg_lo:[0,1] neg_hi:[0,1]
	v_pk_add_f32 v[50:51], v[24:25], v[58:59]
	v_pk_add_f32 v[24:25], v[24:25], v[58:59] neg_lo:[0,1] neg_hi:[0,1]
	v_pk_add_f32 v[28:29], v[44:45], v[78:79]
	v_pk_add_f32 v[58:59], v[44:45], v[78:79] neg_lo:[0,1] neg_hi:[0,1]
	v_pk_add_f32 v[44:45], v[38:39], v[20:21]
	v_pk_add_f32 v[20:21], v[38:39], v[20:21] neg_lo:[0,1] neg_hi:[0,1]
	v_pk_add_f32 v[78:79], v[28:29], v[44:45]
	v_pk_add_f32 v[28:29], v[28:29], v[44:45] neg_lo:[0,1] neg_hi:[0,1]
	v_pk_add_f32 v[44:45], v[58:59], v[20:21] op_sel:[0,1] op_sel_hi:[1,0] neg_hi:[0,1]
	v_pk_add_f32 v[20:21], v[58:59], v[20:21] op_sel:[0,1] op_sel_hi:[1,0] neg_lo:[0,1]
	v_pk_add_f32 v[38:39], v[68:69], v[54:55]
	v_pk_add_f32 v[58:59], v[68:69], v[54:55] neg_lo:[0,1] neg_hi:[0,1]
	v_pk_add_f32 v[54:55], v[76:77], v[52:53]
	v_pk_add_f32 v[52:53], v[76:77], v[52:53] neg_lo:[0,1] neg_hi:[0,1]
	s_nop 0
	v_pk_mul_f32 v[68:69], v[36:37], v[52:53] op_sel:[0,1] op_sel_hi:[0,0] neg_lo:[1,1] neg_hi:[1,0]
	v_pk_fma_f32 v[52:53], v[32:33], v[52:53], v[68:69] op_sel_hi:[0,1,1]
	v_pk_add_f32 v[68:69], v[74:75], v[86:87]
	v_pk_add_f32 v[74:75], v[74:75], v[86:87] neg_lo:[0,1] neg_hi:[0,1]
	s_nop 0
	v_pk_mul_f32 v[76:77], v[10:11], v[74:75] op_sel:[0,1] op_sel_hi:[0,0] neg_lo:[1,1] neg_hi:[1,0]
	v_pk_fma_f32 v[74:75], v[10:11], v[74:75], v[76:77] op_sel_hi:[0,1,1]
	v_pk_add_f32 v[76:77], v[72:73], v[42:43]
	v_pk_add_f32 v[42:43], v[72:73], v[42:43] neg_lo:[0,1] neg_hi:[0,1]
	s_nop 0
	v_pk_mul_f32 v[72:73], v[32:33], v[42:43] op_sel:[0,1] op_sel_hi:[0,0] neg_lo:[1,1] neg_hi:[1,0]
	v_pk_fma_f32 v[42:43], v[36:37], v[42:43], v[72:73] op_sel_hi:[0,1,1]
	v_pk_add_f32 v[72:73], v[56:57], v[88:89]
	v_pk_add_f32 v[56:57], v[56:57], v[88:89] neg_lo:[0,1] neg_hi:[0,1]
	s_nop 0
	v_xor_b32_e32 v83, 0x80000000, v56
	v_mov_b32_e32 v82, v57
	v_pk_add_f32 v[56:57], v[66:67], v[90:91]
	v_pk_add_f32 v[66:67], v[66:67], v[90:91] neg_lo:[0,1] neg_hi:[0,1]
	s_nop 0
	v_pk_mul_f32 v[86:87], v[32:33], v[66:67] op_sel:[0,1] op_sel_hi:[0,0] neg_lo:[1,1] neg_hi:[1,0]
	v_pk_fma_f32 v[66:67], v[36:37], v[66:67], v[86:87] op_sel_hi:[0,1,1] neg_lo:[1,0,0] neg_hi:[1,0,0]
	v_pk_add_f32 v[86:87], v[60:61], v[64:65]
	v_pk_add_f32 v[60:61], v[60:61], v[64:65] neg_lo:[0,1] neg_hi:[0,1]
	s_nop 0
	v_pk_mul_f32 v[64:65], v[10:11], v[60:61] op_sel:[0,1] op_sel_hi:[0,0] neg_lo:[1,1] neg_hi:[1,0]
	v_pk_fma_f32 v[60:61], v[10:11], v[60:61], v[64:65] op_sel_hi:[0,1,1] neg_lo:[1,0,0] neg_hi:[1,0,0]
	v_pk_add_f32 v[64:65], v[48:49], v[62:63]
	v_pk_add_f32 v[48:49], v[48:49], v[62:63] neg_lo:[0,1] neg_hi:[0,1]
	s_nop 0
	v_pk_mul_f32 v[36:37], v[36:37], v[48:49] op_sel:[0,1] op_sel_hi:[0,0] neg_lo:[1,1] neg_hi:[1,0]
	v_pk_fma_f32 v[36:37], v[32:33], v[48:49], v[36:37] op_sel_hi:[0,1,1] neg_lo:[1,0,0] neg_hi:[1,0,0]
	v_pk_add_f32 v[32:33], v[38:39], v[72:73]
	v_pk_add_f32 v[48:49], v[38:39], v[72:73] neg_lo:[0,1] neg_hi:[0,1]
	v_pk_add_f32 v[38:39], v[56:57], v[54:55]
	v_pk_add_f32 v[54:55], v[54:55], v[56:57] neg_lo:[0,1] neg_hi:[0,1]
	v_pk_add_f32 v[62:63], v[68:69], v[86:87] neg_lo:[0,1] neg_hi:[0,1]
	v_pk_mul_f32 v[56:57], v[10:11], v[54:55] op_sel:[0,1] op_sel_hi:[0,0] neg_lo:[1,1] neg_hi:[1,0]
	v_pk_fma_f32 v[56:57], v[10:11], v[54:55], v[56:57] op_sel_hi:[0,1,1]
	v_pk_add_f32 v[54:55], v[68:69], v[86:87]
	v_xor_b32_e32 v69, 0x80000000, v62
	v_mov_b32_e32 v68, v63
	v_pk_add_f32 v[62:63], v[76:77], v[64:65]
	v_pk_add_f32 v[64:65], v[76:77], v[64:65] neg_lo:[0,1] neg_hi:[0,1]
	s_nop 0
	v_pk_mul_f32 v[72:73], v[10:11], v[64:65] op_sel:[0,1] op_sel_hi:[0,0] neg_lo:[1,1] neg_hi:[1,0]
	v_pk_fma_f32 v[64:65], v[10:11], v[64:65], v[72:73] op_sel_hi:[0,1,1] neg_lo:[1,0,0] neg_hi:[1,0,0]
	v_pk_add_f32 v[72:73], v[32:33], v[54:55]
	v_pk_add_f32 v[32:33], v[32:33], v[54:55] neg_lo:[0,1] neg_hi:[0,1]
	v_pk_add_f32 v[54:55], v[38:39], v[62:63]
	v_pk_add_f32 v[38:39], v[38:39], v[62:63] neg_lo:[0,1] neg_hi:[0,1]
	v_pk_add_f32 v[76:77], v[72:73], v[54:55]
	v_pk_add_f32 v[54:55], v[72:73], v[54:55] neg_lo:[0,1] neg_hi:[0,1]
	v_pk_add_f32 v[72:73], v[32:33], v[38:39] op_sel:[0,1] op_sel_hi:[1,0] neg_hi:[0,1]
	v_pk_add_f32 v[38:39], v[32:33], v[38:39] op_sel:[0,1] op_sel_hi:[1,0] neg_lo:[0,1]
	v_pk_add_f32 v[32:33], v[48:49], v[68:69]
	v_pk_add_f32 v[62:63], v[48:49], v[68:69] neg_lo:[0,1] neg_hi:[0,1]
	v_pk_add_f32 v[48:49], v[56:57], v[64:65]
	v_pk_add_f32 v[56:57], v[56:57], v[64:65] neg_lo:[0,1] neg_hi:[0,1]
	s_nop 0
	v_xor_b32_e32 v65, 0x80000000, v56
	v_mov_b32_e32 v64, v57
	v_pk_add_f32 v[56:57], v[32:33], v[48:49]
	v_pk_add_f32 v[48:49], v[32:33], v[48:49] neg_lo:[0,1] neg_hi:[0,1]
	v_pk_add_f32 v[68:69], v[62:63], v[64:65]
	v_pk_add_f32 v[32:33], v[62:63], v[64:65] neg_lo:[0,1] neg_hi:[0,1]
	v_pk_add_f32 v[64:65], v[66:67], v[52:53]
	v_pk_add_f32 v[52:53], v[52:53], v[66:67] neg_lo:[0,1] neg_hi:[0,1]
	v_pk_add_f32 v[62:63], v[58:59], v[82:83]
	v_pk_mul_f32 v[66:67], v[10:11], v[52:53] op_sel:[0,1] op_sel_hi:[0,0] neg_lo:[1,1] neg_hi:[1,0]
	v_pk_fma_f32 v[52:53], v[10:11], v[52:53], v[66:67] op_sel_hi:[0,1,1]
	v_pk_add_f32 v[66:67], v[74:75], v[60:61]
	v_pk_add_f32 v[60:61], v[74:75], v[60:61] neg_lo:[0,1] neg_hi:[0,1]
	v_pk_add_f32 v[58:59], v[58:59], v[82:83] neg_lo:[0,1] neg_hi:[0,1]
	v_xor_b32_e32 v75, 0x80000000, v60
	v_mov_b32_e32 v74, v61
	v_pk_add_f32 v[60:61], v[42:43], v[36:37]
	v_pk_add_f32 v[36:37], v[42:43], v[36:37] neg_lo:[0,1] neg_hi:[0,1]
	s_nop 0
	v_pk_mul_f32 v[42:43], v[10:11], v[36:37] op_sel:[0,1] op_sel_hi:[0,0] neg_lo:[1,1] neg_hi:[1,0]
	v_pk_fma_f32 v[36:37], v[10:11], v[36:37], v[42:43] op_sel_hi:[0,1,1] neg_lo:[1,0,0] neg_hi:[1,0,0]
	v_pk_add_f32 v[42:43], v[62:63], v[66:67]
	v_pk_add_f32 v[62:63], v[62:63], v[66:67] neg_lo:[0,1] neg_hi:[0,1]
	v_pk_add_f32 v[66:67], v[64:65], v[60:61]
	v_pk_add_f32 v[60:61], v[64:65], v[60:61] neg_lo:[0,1] neg_hi:[0,1]
	v_lshl_add_u32 v10, v13, 3, 0
	v_xor_b32_e32 v65, 0x80000000, v60
	v_mov_b32_e32 v64, v61
	v_pk_add_f32 v[60:61], v[42:43], v[66:67]
	v_pk_add_f32 v[66:67], v[42:43], v[66:67] neg_lo:[0,1] neg_hi:[0,1]
	v_pk_add_f32 v[82:83], v[62:63], v[64:65]
	v_pk_add_f32 v[42:43], v[62:63], v[64:65] neg_lo:[0,1] neg_hi:[0,1]
	v_pk_add_f32 v[64:65], v[52:53], v[36:37]
	v_pk_add_f32 v[36:37], v[52:53], v[36:37] neg_lo:[0,1] neg_hi:[0,1]
	v_pk_add_f32 v[62:63], v[58:59], v[74:75]
	v_pk_add_f32 v[58:59], v[58:59], v[74:75] neg_lo:[0,1] neg_hi:[0,1]
	v_pk_add_f32 v[86:87], v[62:63], v[64:65]
	v_pk_add_f32 v[52:53], v[62:63], v[64:65] neg_lo:[0,1] neg_hi:[0,1]
	v_pk_add_f32 v[62:63], v[58:59], v[36:37] op_sel:[0,1] op_sel_hi:[1,0] neg_hi:[0,1]
	v_pk_add_f32 v[36:37], v[58:59], v[36:37] op_sel:[0,1] op_sel_hi:[1,0] neg_lo:[0,1]
	v_pk_mul_f32 v[58:59], v[84:85], s[14:15] op_sel:[1,0] neg_lo:[1,0]
	s_nop 0
	v_pk_fma_f32 v[58:59], v[84:85], s[42:43], v[58:59] op_sel_hi:[0,1,1]
	ds_write_b64 v10, v[58:59]
	v_pk_fma_f32 v[58:59], v[180:181], s[92:93], v[180:181] op_sel:[1,0,0] op_sel_hi:[0,1,1]
	v_pk_mul_f32 v[64:65], v[58:59], v[76:77] op_sel:[1,1] op_sel_hi:[0,1] neg_lo:[0,1]
	v_pk_fma_f32 v[64:65], v[58:59], v[76:77], v[64:65] op_sel_hi:[1,0,1]
	ds_write_b64 v10, v[64:65] offset:4224
	v_pk_mul_f32 v[64:65], v[180:181], v[58:59] op_sel:[1,1] op_sel_hi:[0,1] neg_lo:[0,1]
	v_pk_fma_f32 v[58:59], v[180:181], v[58:59], v[64:65] op_sel_hi:[1,0,1]
	s_nop 0
	v_pk_mul_f32 v[64:65], v[58:59], v[80:81] op_sel:[1,1] op_sel_hi:[0,1] neg_lo:[0,1]
	v_pk_fma_f32 v[64:65], v[58:59], v[80:81], v[64:65] op_sel_hi:[1,0,1]
	ds_write_b64 v10, v[64:65] offset:8448
	v_pk_mul_f32 v[64:65], v[180:181], v[58:59] op_sel:[1,1] op_sel_hi:[0,1] neg_lo:[0,1]
	v_pk_fma_f32 v[58:59], v[180:181], v[58:59], v[64:65] op_sel_hi:[1,0,1]
	s_nop 0
	v_pk_mul_f32 v[64:65], v[58:59], v[60:61] op_sel:[1,1] op_sel_hi:[0,1] neg_lo:[0,1]
	v_pk_fma_f32 v[60:61], v[58:59], v[60:61], v[64:65] op_sel_hi:[1,0,1]
	ds_write_b64 v10, v[60:61] offset:12672
	v_pk_mul_f32 v[60:61], v[180:181], v[58:59] op_sel:[1,1] op_sel_hi:[0,1] neg_lo:[0,1]
	v_pk_fma_f32 v[58:59], v[180:181], v[58:59], v[60:61] op_sel_hi:[1,0,1]
	s_nop 0
	v_pk_mul_f32 v[60:61], v[70:71], v[58:59] op_sel:[1,1] op_sel_hi:[1,0] neg_lo:[1,0]
	s_nop 0
	v_pk_fma_f32 v[60:61], v[70:71], v[58:59], v[60:61] op_sel_hi:[0,1,1]
	ds_write_b64 v10, v[60:61] offset:16896
	v_pk_mul_f32 v[60:61], v[180:181], v[58:59] op_sel:[1,1] op_sel_hi:[0,1] neg_lo:[0,1]
	v_pk_fma_f32 v[58:59], v[180:181], v[58:59], v[60:61] op_sel_hi:[1,0,1]
	s_nop 0
	v_pk_mul_f32 v[60:61], v[58:59], v[56:57] op_sel:[1,1] op_sel_hi:[0,1] neg_lo:[0,1]
	v_pk_fma_f32 v[56:57], v[58:59], v[56:57], v[60:61] op_sel_hi:[1,0,1]
	ds_write_b64 v10, v[56:57] offset:21120
	v_pk_mul_f32 v[56:57], v[180:181], v[58:59] op_sel:[1,1] op_sel_hi:[0,1] neg_lo:[0,1]
	v_pk_fma_f32 v[56:57], v[180:181], v[58:59], v[56:57] op_sel_hi:[1,0,1]
	s_nop 0
	v_pk_mul_f32 v[58:59], v[78:79], v[56:57] op_sel:[1,1] op_sel_hi:[1,0] neg_lo:[1,0]
	s_nop 0
	v_pk_fma_f32 v[58:59], v[78:79], v[56:57], v[58:59] op_sel_hi:[0,1,1]
	ds_write_b64 v10, v[58:59] offset:25344
	v_pk_mul_f32 v[58:59], v[180:181], v[56:57] op_sel:[1,1] op_sel_hi:[0,1] neg_lo:[0,1]
	v_pk_fma_f32 v[56:57], v[180:181], v[56:57], v[58:59] op_sel_hi:[1,0,1]
	s_nop 0
	v_pk_mul_f32 v[58:59], v[86:87], v[56:57] op_sel:[1,1] op_sel_hi:[1,0] neg_lo:[1,0]
	s_nop 0
	v_pk_fma_f32 v[58:59], v[86:87], v[56:57], v[58:59] op_sel_hi:[0,1,1]
	ds_write_b64 v10, v[58:59] offset:29568
	v_pk_mul_f32 v[58:59], v[180:181], v[56:57] op_sel:[1,1] op_sel_hi:[0,1] neg_lo:[0,1]
	v_pk_fma_f32 v[56:57], v[180:181], v[56:57], v[58:59] op_sel_hi:[1,0,1]
	s_nop 0
	v_pk_mul_f32 v[58:59], v[46:47], v[56:57] op_sel:[1,1] op_sel_hi:[1,0] neg_lo:[1,0]
	s_nop 0
	v_pk_fma_f32 v[46:47], v[46:47], v[56:57], v[58:59] op_sel_hi:[0,1,1]
	ds_write_b64 v10, v[46:47] offset:33792
	v_pk_mul_f32 v[46:47], v[180:181], v[56:57] op_sel:[1,1] op_sel_hi:[0,1] neg_lo:[0,1]
	v_pk_fma_f32 v[46:47], v[180:181], v[56:57], v[46:47] op_sel_hi:[1,0,1]
	s_nop 0
	v_pk_mul_f32 v[56:57], v[72:73], v[46:47] op_sel:[1,1] op_sel_hi:[1,0] neg_lo:[1,0]
	s_nop 0
	v_pk_fma_f32 v[56:57], v[72:73], v[46:47], v[56:57] op_sel_hi:[0,1,1]
	ds_write_b64 v10, v[56:57] offset:38016
	v_pk_mul_f32 v[56:57], v[180:181], v[46:47] op_sel:[1,1] op_sel_hi:[0,1] neg_lo:[0,1]
	v_pk_fma_f32 v[46:47], v[180:181], v[46:47], v[56:57] op_sel_hi:[1,0,1]
	s_nop 0
	v_pk_mul_f32 v[56:57], v[50:51], v[46:47] op_sel:[1,1] op_sel_hi:[1,0] neg_lo:[1,0]
	s_nop 0
	v_pk_fma_f32 v[50:51], v[50:51], v[46:47], v[56:57] op_sel_hi:[0,1,1]
	ds_write_b64 v10, v[50:51] offset:42240
	v_pk_mul_f32 v[50:51], v[180:181], v[46:47] op_sel:[1,1] op_sel_hi:[0,1] neg_lo:[0,1]
	v_pk_fma_f32 v[46:47], v[180:181], v[46:47], v[50:51] op_sel_hi:[1,0,1]
	s_nop 0
	v_pk_mul_f32 v[50:51], v[82:83], v[46:47] op_sel:[1,1] op_sel_hi:[1,0] neg_lo:[1,0]
	s_nop 0
	v_pk_fma_f32 v[50:51], v[82:83], v[46:47], v[50:51] op_sel_hi:[0,1,1]
	ds_write_b64 v10, v[50:51] offset:46464
	v_pk_mul_f32 v[50:51], v[180:181], v[46:47] op_sel:[1,1] op_sel_hi:[0,1] neg_lo:[0,1]
	v_pk_fma_f32 v[46:47], v[180:181], v[46:47], v[50:51] op_sel_hi:[1,0,1]
	s_nop 0
	v_pk_mul_f32 v[50:51], v[40:41], v[46:47] op_sel:[1,1] op_sel_hi:[1,0] neg_lo:[1,0]
	s_nop 0
	v_pk_fma_f32 v[40:41], v[40:41], v[46:47], v[50:51] op_sel_hi:[0,1,1]
	ds_write_b64 v10, v[40:41] offset:50688
	v_pk_mul_f32 v[40:41], v[180:181], v[46:47] op_sel:[1,1] op_sel_hi:[0,1] neg_lo:[0,1]
	v_pk_fma_f32 v[40:41], v[180:181], v[46:47], v[40:41] op_sel_hi:[1,0,1]
	s_nop 0
	v_pk_mul_f32 v[46:47], v[68:69], v[40:41] op_sel:[1,1] op_sel_hi:[1,0] neg_lo:[1,0]
	s_nop 0
	v_pk_fma_f32 v[46:47], v[68:69], v[40:41], v[46:47] op_sel_hi:[0,1,1]
	ds_write_b64 v10, v[46:47] offset:54912
	v_pk_mul_f32 v[46:47], v[180:181], v[40:41] op_sel:[1,1] op_sel_hi:[0,1] neg_lo:[0,1]
	v_pk_fma_f32 v[40:41], v[180:181], v[40:41], v[46:47] op_sel_hi:[1,0,1]
	s_nop 0
	v_pk_mul_f32 v[46:47], v[44:45], v[40:41] op_sel:[1,1] op_sel_hi:[1,0] neg_lo:[1,0]
	s_nop 0
	v_pk_fma_f32 v[44:45], v[44:45], v[40:41], v[46:47] op_sel_hi:[0,1,1]
	ds_write_b64 v10, v[44:45] offset:59136
	v_pk_mul_f32 v[44:45], v[180:181], v[40:41] op_sel:[1,1] op_sel_hi:[0,1] neg_lo:[0,1]
	v_pk_fma_f32 v[40:41], v[180:181], v[40:41], v[44:45] op_sel_hi:[1,0,1]
	s_nop 0
	v_pk_mul_f32 v[44:45], v[62:63], v[40:41] op_sel:[1,1] op_sel_hi:[1,0] neg_lo:[1,0]
	s_nop 0
	v_pk_fma_f32 v[44:45], v[62:63], v[40:41], v[44:45] op_sel_hi:[0,1,1]
	ds_write_b64 v10, v[44:45] offset:63360
	v_pk_mul_f32 v[44:45], v[180:181], v[40:41] op_sel:[1,1] op_sel_hi:[0,1] neg_lo:[0,1]
	v_pk_fma_f32 v[40:41], v[180:181], v[40:41], v[44:45] op_sel_hi:[1,0,1]
	s_nop 0
	v_pk_mul_f32 v[44:45], v[30:31], v[40:41] op_sel:[1,1] op_sel_hi:[1,0] neg_lo:[1,0]
	v_add_u32_e32 v13, 0x10800, v10
	v_pk_fma_f32 v[30:31], v[30:31], v[40:41], v[44:45] op_sel_hi:[0,1,1]
	ds_write_b64 v13, v[30:31]
	v_pk_mul_f32 v[30:31], v[180:181], v[40:41] op_sel:[1,1] op_sel_hi:[0,1] neg_lo:[0,1]
	v_pk_fma_f32 v[30:31], v[180:181], v[40:41], v[30:31] op_sel_hi:[1,0,1]
	s_nop 0
	v_pk_mul_f32 v[40:41], v[54:55], v[30:31] op_sel:[1,1] op_sel_hi:[1,0] neg_lo:[1,0]
	v_add_u32_e32 v13, 0x11880, v10
	v_pk_fma_f32 v[40:41], v[54:55], v[30:31], v[40:41] op_sel_hi:[0,1,1]
	ds_write_b64 v13, v[40:41]
	v_pk_mul_f32 v[40:41], v[180:181], v[30:31] op_sel:[1,1] op_sel_hi:[0,1] neg_lo:[0,1]
	v_pk_fma_f32 v[30:31], v[180:181], v[30:31], v[40:41] op_sel_hi:[1,0,1]
	s_nop 0
	v_pk_mul_f32 v[40:41], v[34:35], v[30:31] op_sel:[1,1] op_sel_hi:[1,0] neg_lo:[1,0]
	v_add_u32_e32 v13, 0x12900, v10
	v_pk_fma_f32 v[34:35], v[34:35], v[30:31], v[40:41] op_sel_hi:[0,1,1]
	ds_write_b64 v13, v[34:35]
	v_pk_mul_f32 v[34:35], v[180:181], v[30:31] op_sel:[1,1] op_sel_hi:[0,1] neg_lo:[0,1]
	v_pk_fma_f32 v[30:31], v[180:181], v[30:31], v[34:35] op_sel_hi:[1,0,1]
	s_nop 0
	v_pk_mul_f32 v[34:35], v[66:67], v[30:31] op_sel:[1,1] op_sel_hi:[1,0] neg_lo:[1,0]
	v_add_u32_e32 v13, 0x13980, v10
	v_pk_fma_f32 v[34:35], v[66:67], v[30:31], v[34:35] op_sel_hi:[0,1,1]
	ds_write_b64 v13, v[34:35]
	v_pk_mul_f32 v[34:35], v[180:181], v[30:31] op_sel:[1,1] op_sel_hi:[0,1] neg_lo:[0,1]
	v_pk_fma_f32 v[30:31], v[180:181], v[30:31], v[34:35] op_sel_hi:[1,0,1]
	s_nop 0
	v_pk_mul_f32 v[34:35], v[26:27], v[30:31] op_sel:[1,1] op_sel_hi:[1,0] neg_lo:[1,0]
	v_add_u32_e32 v13, 0x14a00, v10
	v_pk_fma_f32 v[26:27], v[26:27], v[30:31], v[34:35] op_sel_hi:[0,1,1]
	ds_write_b64 v13, v[26:27]
	v_pk_mul_f32 v[26:27], v[180:181], v[30:31] op_sel:[1,1] op_sel_hi:[0,1] neg_lo:[0,1]
	v_pk_fma_f32 v[26:27], v[180:181], v[30:31], v[26:27] op_sel_hi:[1,0,1]
	s_nop 0
	v_pk_mul_f32 v[30:31], v[48:49], v[26:27] op_sel:[1,1] op_sel_hi:[1,0] neg_lo:[1,0]
	v_add_u32_e32 v13, 0x15a80, v10
	v_pk_fma_f32 v[30:31], v[48:49], v[26:27], v[30:31] op_sel_hi:[0,1,1]
	ds_write_b64 v13, v[30:31]
	v_pk_mul_f32 v[30:31], v[180:181], v[26:27] op_sel:[1,1] op_sel_hi:[0,1] neg_lo:[0,1]
	v_pk_fma_f32 v[26:27], v[180:181], v[26:27], v[30:31] op_sel_hi:[1,0,1]
	s_nop 0
	v_pk_mul_f32 v[30:31], v[28:29], v[26:27] op_sel:[1,1] op_sel_hi:[1,0] neg_lo:[1,0]
	v_add_u32_e32 v13, 0x16b00, v10
	v_pk_fma_f32 v[28:29], v[28:29], v[26:27], v[30:31] op_sel_hi:[0,1,1]
	ds_write_b64 v13, v[28:29]
	v_pk_mul_f32 v[28:29], v[180:181], v[26:27] op_sel:[1,1] op_sel_hi:[0,1] neg_lo:[0,1]
	v_pk_fma_f32 v[26:27], v[180:181], v[26:27], v[28:29] op_sel_hi:[1,0,1]
	s_nop 0
	v_pk_mul_f32 v[28:29], v[52:53], v[26:27] op_sel:[1,1] op_sel_hi:[1,0] neg_lo:[1,0]
	v_add_u32_e32 v13, 0x17b80, v10
	v_pk_fma_f32 v[28:29], v[52:53], v[26:27], v[28:29] op_sel_hi:[0,1,1]
	ds_write_b64 v13, v[28:29]
	v_pk_mul_f32 v[28:29], v[180:181], v[26:27] op_sel:[1,1] op_sel_hi:[0,1] neg_lo:[0,1]
	v_pk_fma_f32 v[26:27], v[180:181], v[26:27], v[28:29] op_sel_hi:[1,0,1]
	s_nop 0
	v_pk_mul_f32 v[28:29], v[22:23], v[26:27] op_sel:[1,1] op_sel_hi:[1,0] neg_lo:[1,0]
	v_add_u32_e32 v13, 0x18c00, v10
	v_pk_fma_f32 v[22:23], v[22:23], v[26:27], v[28:29] op_sel_hi:[0,1,1]
	ds_write_b64 v13, v[22:23]
	v_pk_mul_f32 v[22:23], v[180:181], v[26:27] op_sel:[1,1] op_sel_hi:[0,1] neg_lo:[0,1]
	v_pk_fma_f32 v[22:23], v[180:181], v[26:27], v[22:23] op_sel_hi:[1,0,1]
	s_nop 0
	v_pk_mul_f32 v[26:27], v[38:39], v[22:23] op_sel:[1,1] op_sel_hi:[1,0] neg_lo:[1,0]
	v_add_u32_e32 v13, 0x19c80, v10
	v_pk_fma_f32 v[26:27], v[38:39], v[22:23], v[26:27] op_sel_hi:[0,1,1]
	ds_write_b64 v13, v[26:27]
	v_pk_mul_f32 v[26:27], v[180:181], v[22:23] op_sel:[1,1] op_sel_hi:[0,1] neg_lo:[0,1]
	v_pk_fma_f32 v[22:23], v[180:181], v[22:23], v[26:27] op_sel_hi:[1,0,1]
	s_nop 0
	v_pk_mul_f32 v[26:27], v[24:25], v[22:23] op_sel:[1,1] op_sel_hi:[1,0] neg_lo:[1,0]
	v_add_u32_e32 v13, 0x1ad00, v10
	v_pk_fma_f32 v[24:25], v[24:25], v[22:23], v[26:27] op_sel_hi:[0,1,1]
	ds_write_b64 v13, v[24:25]
	v_pk_mul_f32 v[24:25], v[180:181], v[22:23] op_sel:[1,1] op_sel_hi:[0,1] neg_lo:[0,1]
	v_pk_fma_f32 v[22:23], v[180:181], v[22:23], v[24:25] op_sel_hi:[1,0,1]
	s_nop 0
	v_pk_mul_f32 v[24:25], v[42:43], v[22:23] op_sel:[1,1] op_sel_hi:[1,0] neg_lo:[1,0]
	v_add_u32_e32 v13, 0x1bd80, v10
	v_pk_fma_f32 v[24:25], v[42:43], v[22:23], v[24:25] op_sel_hi:[0,1,1]
	ds_write_b64 v13, v[24:25]
	v_pk_mul_f32 v[24:25], v[180:181], v[22:23] op_sel:[1,1] op_sel_hi:[0,1] neg_lo:[0,1]
	v_pk_fma_f32 v[22:23], v[180:181], v[22:23], v[24:25] op_sel_hi:[1,0,1]
	s_nop 0
	v_pk_mul_f32 v[24:25], v[18:19], v[22:23] op_sel:[1,1] op_sel_hi:[1,0] neg_lo:[1,0]
	v_add_u32_e32 v13, 0x1ce00, v10
	v_pk_fma_f32 v[18:19], v[18:19], v[22:23], v[24:25] op_sel_hi:[0,1,1]
	ds_write_b64 v13, v[18:19]
	v_pk_mul_f32 v[18:19], v[180:181], v[22:23] op_sel:[1,1] op_sel_hi:[0,1] neg_lo:[0,1]
	v_pk_fma_f32 v[18:19], v[180:181], v[22:23], v[18:19] op_sel_hi:[1,0,1]
	s_nop 0
	v_pk_mul_f32 v[22:23], v[32:33], v[18:19] op_sel:[1,1] op_sel_hi:[1,0] neg_lo:[1,0]
	v_add_u32_e32 v13, 0x1de80, v10
	v_pk_fma_f32 v[22:23], v[32:33], v[18:19], v[22:23] op_sel_hi:[0,1,1]
	ds_write_b64 v13, v[22:23]
	v_pk_mul_f32 v[22:23], v[180:181], v[18:19] op_sel:[1,1] op_sel_hi:[0,1] neg_lo:[0,1]
	v_pk_fma_f32 v[18:19], v[180:181], v[18:19], v[22:23] op_sel_hi:[1,0,1]
	s_nop 0
	v_pk_mul_f32 v[22:23], v[20:21], v[18:19] op_sel:[1,1] op_sel_hi:[1,0] neg_lo:[1,0]
	v_add_u32_e32 v13, 0x1ef00, v10
	v_pk_fma_f32 v[20:21], v[20:21], v[18:19], v[22:23] op_sel_hi:[0,1,1]
	ds_write_b64 v13, v[20:21]
	v_pk_mul_f32 v[20:21], v[180:181], v[18:19] op_sel:[1,1] op_sel_hi:[0,1] neg_lo:[0,1]
	v_pk_fma_f32 v[16:17], v[180:181], v[18:19], v[20:21] op_sel_hi:[1,0,1]
	s_nop 0
	v_pk_mul_f32 v[18:19], v[36:37], v[16:17] op_sel:[1,1] op_sel_hi:[1,0] neg_lo:[1,0]
	v_add_u32_e32 v10, 0x1ff80, v10
	v_pk_fma_f32 v[16:17], v[36:37], v[16:17], v[18:19] op_sel_hi:[0,1,1]
	ds_write_b64 v10, v[16:17]
	v_mov_b32_e32 v10, v176
	v_mov_b32_e32 v13, v173
	s_waitcnt lgkmcnt(0)
	s_barrier
	v_mov_b32_e32 v16, v182
	v_add_u32_e32 v15, v13, v10
	v_lshl_add_u32 v75, v15, 3, 0
	v_xad_u32 v15, v13, 1, v10
	v_lshl_add_u32 v74, v15, 3, 0
	v_xad_u32 v15, v13, 2, v10
	v_lshl_add_u32 v73, v15, 3, 0
	v_xad_u32 v15, v13, 3, v10
	v_lshl_add_u32 v72, v15, 3, 0
	v_xad_u32 v15, v13, 4, v10
	v_lshl_add_u32 v71, v15, 3, 0
	v_xad_u32 v15, v13, 5, v10
	v_lshl_add_u32 v70, v15, 3, 0
	v_xad_u32 v15, v13, 6, v10
	v_lshl_add_u32 v69, v15, 3, 0
	v_xad_u32 v15, v13, 7, v10
	v_lshl_add_u32 v68, v15, 3, 0
	v_xad_u32 v15, v13, 8, v10
	v_lshl_add_u32 v15, v15, 3, 0
	v_add_u32_e32 v67, 0x800, v15
	v_xad_u32 v15, v13, 9, v10
	v_lshl_add_u32 v15, v15, 3, 0
	v_add_u32_e32 v66, 0x800, v15
	v_xad_u32 v15, v13, 10, v10
	v_lshl_add_u32 v15, v15, 3, 0
	v_add_u32_e32 v65, 0x800, v15
	v_xad_u32 v15, v13, 11, v10
	v_lshl_add_u32 v15, v15, 3, 0
	v_add_u32_e32 v64, 0x800, v15
	v_xad_u32 v15, v13, 12, v10
	v_mov_b32_e32 v17, v183
	v_lshl_add_u32 v15, v15, 3, 0
	ds_read2_b64 v[18:21], v75 offset1:16
	ds_read2_b64 v[40:43], v67 offset1:16
	v_add_u32_e32 v63, 0x800, v15
	v_xad_u32 v15, v13, 13, v10
	v_lshl_add_u32 v15, v15, 3, 0
	v_add_u32_e32 v62, 0x800, v15
	v_xad_u32 v15, v13, 14, v10
	v_xad_u32 v10, v13, 15, v10
	ds_read2_b64 v[22:25], v74 offset0:32 offset1:48
	ds_read2_b64 v[48:51], v66 offset0:32 offset1:48
	v_lshl_add_u32 v15, v15, 3, 0
	v_lshl_add_u32 v10, v10, 3, 0
	v_add_u32_e32 v15, 0x800, v15
	v_add_u32_e32 v13, 0x800, v10
	ds_read2_b64 v[26:29], v73 offset0:64 offset1:80
	ds_read2_b64 v[58:61], v72 offset0:96 offset1:112
	ds_read2_b64 v[76:79], v71 offset0:128 offset1:144
	ds_read2_b64 v[80:83], v70 offset0:160 offset1:176
	ds_read2_b64 v[84:87], v69 offset0:192 offset1:208
	ds_read2_b64 v[88:91], v68 offset0:224 offset1:240
	ds_read2_b64 v[54:57], v65 offset0:64 offset1:80
	ds_read2_b64 v[92:95], v64 offset0:96 offset1:112
	ds_read2_b64 v[96:99], v63 offset0:128 offset1:144
	ds_read2_b64 v[100:103], v62 offset0:160 offset1:176
	ds_read2_b64 v[104:107], v15 offset0:192 offset1:208
	ds_read2_b64 v[108:111], v13 offset0:224 offset1:240
	s_waitcnt lgkmcnt(14)
	v_pk_add_f32 v[112:113], v[18:19], v[40:41]
	v_pk_add_f32 v[40:41], v[18:19], v[40:41] neg_lo:[0,1] neg_hi:[0,1]
	v_pk_add_f32 v[18:19], v[20:21], v[42:43]
	v_pk_add_f32 v[20:21], v[20:21], v[42:43] neg_lo:[0,1] neg_hi:[0,1]
	v_mov_b32_e32 v30, v165
	v_mov_b32_e32 v32, v166
	v_mov_b32_e32 v34, v167
	v_mov_b32_e32 v10, v168
	v_mov_b32_e32 v38, v169
	v_mov_b32_e32 v36, v170
	v_mov_b32_e32 v46, v171
	v_mov_b32_e32 v31, v172
	v_pk_mul_f32 v[42:43], v[20:21], v[46:47] op_sel:[1,0] op_sel_hi:[0,0] neg_lo:[1,1] neg_hi:[0,1]
	s_nop 0
	v_pk_fma_f32 v[44:45], v[20:21], v[30:31], v[42:43] op_sel_hi:[1,0,1]
	s_waitcnt lgkmcnt(12)
	v_pk_add_f32 v[20:21], v[22:23], v[48:49]
	v_pk_add_f32 v[22:23], v[22:23], v[48:49] neg_lo:[0,1] neg_hi:[0,1]
	s_nop 0
	v_pk_mul_f32 v[42:43], v[22:23], v[36:37] op_sel:[1,0] op_sel_hi:[0,0] neg_lo:[1,1] neg_hi:[0,1]
	s_nop 0
	v_pk_fma_f32 v[48:49], v[22:23], v[32:33], v[42:43] op_sel_hi:[1,0,1]
	v_pk_add_f32 v[22:23], v[24:25], v[50:51]
	v_pk_add_f32 v[24:25], v[24:25], v[50:51] neg_lo:[0,1] neg_hi:[0,1]
	s_nop 0
	v_pk_mul_f32 v[42:43], v[24:25], v[38:39] op_sel:[1,0] op_sel_hi:[0,0] neg_lo:[1,1] neg_hi:[0,1]
	s_nop 0
	v_pk_fma_f32 v[52:53], v[24:25], v[34:35], v[42:43] op_sel_hi:[1,0,1]
	s_waitcnt lgkmcnt(5)
	v_pk_add_f32 v[24:25], v[26:27], v[54:55]
	v_pk_add_f32 v[26:27], v[26:27], v[54:55] neg_lo:[0,1] neg_hi:[0,1]
	s_nop 0
	v_pk_mul_f32 v[42:43], v[26:27], v[10:11] op_sel:[1,0] op_sel_hi:[0,0] neg_lo:[1,1] neg_hi:[0,1]
	s_nop 0
	v_pk_fma_f32 v[54:55], v[26:27], v[10:11], v[42:43] op_sel_hi:[1,0,1]
	v_pk_add_f32 v[26:27], v[28:29], v[56:57]
	v_pk_add_f32 v[28:29], v[28:29], v[56:57] neg_lo:[0,1] neg_hi:[0,1]
	s_nop 0
	v_pk_mul_f32 v[42:43], v[28:29], v[38:39] op_sel_hi:[1,0]
	s_nop 0
	v_pk_fma_f32 v[56:57], v[28:29], v[34:35], v[42:43] op_sel:[1,0,0] op_sel_hi:[0,0,1] neg_lo:[1,1,0] neg_hi:[0,1,0]
	s_waitcnt lgkmcnt(4)
	v_pk_add_f32 v[42:43], v[58:59], v[92:93] neg_lo:[0,1] neg_hi:[0,1]
	v_pk_add_f32 v[28:29], v[58:59], v[92:93]
	v_pk_mul_f32 v[50:51], v[42:43], v[36:37] op_sel_hi:[1,0]
	s_nop 0
	v_pk_fma_f32 v[58:59], v[42:43], v[32:33], v[50:51] op_sel:[1,0,0] op_sel_hi:[0,0,1] neg_lo:[1,1,0] neg_hi:[0,1,0]
	v_pk_add_f32 v[50:51], v[60:61], v[94:95] neg_lo:[0,1] neg_hi:[0,1]
	v_pk_add_f32 v[42:43], v[60:61], v[94:95]
	v_pk_mul_f32 v[60:61], v[50:51], v[46:47] op_sel_hi:[1,0]
	v_xor_b32_e32 v92, 0x80000000, v51
	v_mov_b32_e32 v93, v50
	s_waitcnt lgkmcnt(3)
	v_pk_add_f32 v[50:51], v[76:77], v[96:97]
	v_pk_add_f32 v[76:77], v[76:77], v[96:97] neg_lo:[0,1] neg_hi:[0,1]
	v_pk_fma_f32 v[60:61], v[92:93], v[30:31], v[60:61] op_sel_hi:[1,0,1] neg_lo:[0,1,0] neg_hi:[0,1,0]
	v_xor_b32_e32 v93, 0x80000000, v76
	v_mov_b32_e32 v92, v77
	v_pk_add_f32 v[76:77], v[78:79], v[98:99]
	v_pk_add_f32 v[78:79], v[78:79], v[98:99] neg_lo:[0,1] neg_hi:[0,1]
	s_nop 0
	v_pk_mul_f32 v[94:95], v[78:79], v[46:47] op_sel_hi:[1,0] neg_lo:[0,1] neg_hi:[0,1]
	s_nop 0
	v_pk_fma_f32 v[78:79], v[78:79], v[30:31], v[94:95] op_sel:[1,0,0] op_sel_hi:[0,0,1] neg_lo:[1,1,0] neg_hi:[0,1,0]
	s_waitcnt lgkmcnt(2)
	v_pk_add_f32 v[94:95], v[80:81], v[100:101]
	v_pk_add_f32 v[80:81], v[80:81], v[100:101] neg_lo:[0,1] neg_hi:[0,1]
	s_nop 0
	v_pk_mul_f32 v[96:97], v[80:81], v[36:37] op_sel_hi:[1,0] neg_lo:[0,1] neg_hi:[0,1]
	s_nop 0
	v_pk_fma_f32 v[80:81], v[80:81], v[32:33], v[96:97] op_sel:[1,0,0] op_sel_hi:[0,0,1] neg_lo:[1,1,0] neg_hi:[0,1,0]
	v_pk_add_f32 v[96:97], v[82:83], v[102:103]
	v_pk_add_f32 v[82:83], v[82:83], v[102:103] neg_lo:[0,1] neg_hi:[0,1]
	s_nop 0
	v_pk_mul_f32 v[98:99], v[82:83], v[38:39] op_sel_hi:[1,0] neg_lo:[0,1] neg_hi:[0,1]
	s_nop 0
	v_pk_fma_f32 v[82:83], v[82:83], v[34:35], v[98:99] op_sel:[1,0,0] op_sel_hi:[0,0,1] neg_lo:[1,1,0] neg_hi:[0,1,0]
	s_waitcnt lgkmcnt(1)
	v_pk_add_f32 v[98:99], v[84:85], v[104:105]
	v_pk_add_f32 v[84:85], v[84:85], v[104:105] neg_lo:[0,1] neg_hi:[0,1]
	s_nop 0
	v_pk_mul_f32 v[100:101], v[84:85], v[10:11] op_sel:[1,0] op_sel_hi:[0,0] neg_lo:[1,1] neg_hi:[0,1]
	s_nop 0
	v_pk_fma_f32 v[84:85], v[84:85], v[10:11], v[100:101] op_sel_hi:[1,0,1] neg_lo:[0,1,0] neg_hi:[0,1,0]
	v_pk_add_f32 v[100:101], v[86:87], v[106:107]
	v_pk_add_f32 v[86:87], v[86:87], v[106:107] neg_lo:[0,1] neg_hi:[0,1]
	s_nop 0
	v_pk_mul_f32 v[38:39], v[86:87], v[38:39] op_sel:[1,0] op_sel_hi:[0,0] neg_lo:[1,1] neg_hi:[0,1]
	s_nop 0
	v_pk_fma_f32 v[86:87], v[86:87], v[34:35], v[38:39] op_sel_hi:[1,0,1] neg_lo:[0,1,0] neg_hi:[0,1,0]
	s_waitcnt lgkmcnt(0)
	v_pk_add_f32 v[38:39], v[88:89], v[108:109] neg_lo:[0,1] neg_hi:[0,1]
	v_pk_add_f32 v[34:35], v[88:89], v[108:109]
	v_pk_mul_f32 v[88:89], v[38:39], v[36:37] op_sel:[1,0] op_sel_hi:[0,0] neg_lo:[1,1] neg_hi:[0,1]
	s_nop 0
	v_pk_fma_f32 v[88:89], v[38:39], v[32:33], v[88:89] op_sel_hi:[1,0,1] neg_lo:[0,1,0] neg_hi:[0,1,0]
	v_pk_add_f32 v[38:39], v[90:91], v[110:111]
	v_pk_add_f32 v[90:91], v[90:91], v[110:111] neg_lo:[0,1] neg_hi:[0,1]
	s_nop 0
	v_pk_mul_f32 v[46:47], v[90:91], v[46:47] op_sel:[1,0] op_sel_hi:[0,0] neg_lo:[1,1] neg_hi:[0,1]
	s_nop 0
	v_pk_fma_f32 v[90:91], v[90:91], v[30:31], v[46:47] op_sel_hi:[1,0,1] neg_lo:[0,1,0] neg_hi:[0,1,0]
	v_pk_add_f32 v[46:47], v[18:19], v[76:77]
	v_pk_add_f32 v[18:19], v[18:19], v[76:77] neg_lo:[0,1] neg_hi:[0,1]
	v_pk_add_f32 v[30:31], v[112:113], v[50:51]
	v_pk_mul_f32 v[76:77], v[18:19], v[36:37] op_sel:[1,0] op_sel_hi:[0,0] neg_lo:[1,1] neg_hi:[0,1]
	v_pk_add_f32 v[50:51], v[112:113], v[50:51] neg_lo:[0,1] neg_hi:[0,1]
	v_pk_fma_f32 v[76:77], v[18:19], v[32:33], v[76:77] op_sel_hi:[1,0,1]
	v_pk_add_f32 v[18:19], v[20:21], v[94:95]
	v_pk_add_f32 v[20:21], v[20:21], v[94:95] neg_lo:[0,1] neg_hi:[0,1]
	s_nop 0
	v_pk_mul_f32 v[94:95], v[20:21], v[10:11] op_sel:[1,0] op_sel_hi:[0,0] neg_lo:[1,1] neg_hi:[0,1]
	s_nop 0
	v_pk_fma_f32 v[20:21], v[20:21], v[10:11], v[94:95] op_sel_hi:[1,0,1]
	v_pk_add_f32 v[94:95], v[22:23], v[96:97]
	v_pk_add_f32 v[22:23], v[22:23], v[96:97] neg_lo:[0,1] neg_hi:[0,1]
	s_nop 0
	v_pk_mul_f32 v[96:97], v[22:23], v[36:37] op_sel_hi:[1,0]
	v_xor_b32_e32 v102, 0x80000000, v23
	v_mov_b32_e32 v103, v22
	v_pk_add_f32 v[22:23], v[24:25], v[98:99]
	v_pk_add_f32 v[24:25], v[24:25], v[98:99] neg_lo:[0,1] neg_hi:[0,1]
	v_pk_fma_f32 v[96:97], v[102:103], v[32:33], v[96:97] op_sel_hi:[1,0,1] neg_lo:[0,1,0] neg_hi:[0,1,0]
	v_xor_b32_e32 v99, 0x80000000, v24
	v_mov_b32_e32 v98, v25
	v_pk_add_f32 v[24:25], v[26:27], v[100:101]
	v_pk_add_f32 v[26:27], v[26:27], v[100:101] neg_lo:[0,1] neg_hi:[0,1]
	s_nop 0
	v_pk_mul_f32 v[100:101], v[26:27], v[36:37] op_sel_hi:[1,0] neg_lo:[0,1] neg_hi:[0,1]
	v_xor_b32_e32 v102, 0x80000000, v27
	v_mov_b32_e32 v103, v26
	v_pk_add_f32 v[26:27], v[28:29], v[34:35]
	v_pk_add_f32 v[28:29], v[28:29], v[34:35] neg_lo:[0,1] neg_hi:[0,1]
	v_pk_fma_f32 v[100:101], v[102:103], v[32:33], v[100:101] op_sel_hi:[1,0,1] neg_lo:[0,1,0] neg_hi:[0,1,0]
	v_pk_mul_f32 v[34:35], v[28:29], v[10:11] op_sel:[1,0] op_sel_hi:[0,0] neg_lo:[1,1] neg_hi:[0,1]
	v_pk_add_f32 v[102:103], v[30:31], v[22:23] neg_lo:[0,1] neg_hi:[0,1]
	v_pk_fma_f32 v[28:29], v[28:29], v[10:11], v[34:35] op_sel_hi:[1,0,1] neg_lo:[0,1,0] neg_hi:[0,1,0]
	v_pk_add_f32 v[34:35], v[42:43], v[38:39]
	v_pk_add_f32 v[38:39], v[42:43], v[38:39] neg_lo:[0,1] neg_hi:[0,1]
	s_nop 0
	v_pk_mul_f32 v[42:43], v[38:39], v[36:37] op_sel:[1,0] op_sel_hi:[0,0] neg_lo:[1,1] neg_hi:[0,1]
	s_nop 0
	v_pk_fma_f32 v[42:43], v[38:39], v[32:33], v[42:43] op_sel_hi:[1,0,1] neg_lo:[0,1,0] neg_hi:[0,1,0]
	v_pk_add_f32 v[38:39], v[30:31], v[22:23]
	v_pk_add_f32 v[22:23], v[46:47], v[24:25]
	v_pk_add_f32 v[24:25], v[46:47], v[24:25] neg_lo:[0,1] neg_hi:[0,1]
	s_nop 0
	v_pk_mul_f32 v[30:31], v[24:25], v[10:11] op_sel:[1,0] op_sel_hi:[0,0] neg_lo:[1,1] neg_hi:[0,1]
	s_nop 0
	v_pk_fma_f32 v[24:25], v[24:25], v[10:11], v[30:31] op_sel_hi:[1,0,1]
	v_pk_add_f32 v[30:31], v[18:19], v[26:27]
	v_pk_add_f32 v[18:19], v[18:19], v[26:27] neg_lo:[0,1] neg_hi:[0,1]
	s_nop 0
	v_xor_b32_e32 v27, 0x80000000, v18
	v_mov_b32_e32 v26, v19
	v_pk_add_f32 v[18:19], v[94:95], v[34:35]
	v_pk_add_f32 v[34:35], v[94:95], v[34:35] neg_lo:[0,1] neg_hi:[0,1]
	s_nop 0
	v_pk_mul_f32 v[46:47], v[34:35], v[10:11] op_sel:[1,0] op_sel_hi:[0,0] neg_lo:[1,1] neg_hi:[0,1]
	s_nop 0
	v_pk_fma_f32 v[34:35], v[34:35], v[10:11], v[46:47] op_sel_hi:[1,0,1] neg_lo:[0,1,0] neg_hi:[0,1,0]
	v_pk_add_f32 v[46:47], v[38:39], v[30:31]
	v_pk_add_f32 v[38:39], v[38:39], v[30:31] neg_lo:[0,1] neg_hi:[0,1]
	v_pk_add_f32 v[30:31], v[22:23], v[18:19]
	v_pk_add_f32 v[18:19], v[22:23], v[18:19] neg_lo:[0,1] neg_hi:[0,1]
	v_pk_add_f32 v[94:95], v[46:47], v[30:31]
	v_xor_b32_e32 v23, 0x80000000, v18
	v_mov_b32_e32 v22, v19
	v_pk_add_f32 v[18:19], v[102:103], v[26:27]
	v_pk_add_f32 v[102:103], v[102:103], v[26:27] neg_lo:[0,1] neg_hi:[0,1]
	v_pk_add_f32 v[26:27], v[24:25], v[34:35]
	v_pk_add_f32 v[24:25], v[24:25], v[34:35] neg_lo:[0,1] neg_hi:[0,1]
	v_pk_add_f32 v[30:31], v[46:47], v[30:31] neg_lo:[0,1] neg_hi:[0,1]
	v_xor_b32_e32 v35, 0x80000000, v24
	v_mov_b32_e32 v34, v25
	v_pk_add_f32 v[24:25], v[50:51], v[98:99]
	v_pk_add_f32 v[98:99], v[50:51], v[98:99] neg_lo:[0,1] neg_hi:[0,1]
	v_pk_add_f32 v[50:51], v[76:77], v[100:101] neg_lo:[0,1] neg_hi:[0,1]
	v_pk_add_f32 v[46:47], v[38:39], v[22:23]
	v_pk_add_f32 v[22:23], v[38:39], v[22:23] neg_lo:[0,1] neg_hi:[0,1]
	v_pk_add_f32 v[104:105], v[18:19], v[26:27]
	v_pk_add_f32 v[26:27], v[18:19], v[26:27] neg_lo:[0,1] neg_hi:[0,1]
	v_pk_add_f32 v[38:39], v[102:103], v[34:35]
	v_pk_add_f32 v[18:19], v[102:103], v[34:35] neg_lo:[0,1] neg_hi:[0,1]
	v_pk_add_f32 v[34:35], v[76:77], v[100:101]
	v_pk_mul_f32 v[76:77], v[10:11], v[50:51] op_sel:[0,1] op_sel_hi:[0,0] neg_lo:[1,1] neg_hi:[1,0]
	v_pk_fma_f32 v[76:77], v[10:11], v[50:51], v[76:77] op_sel_hi:[0,1,1]
	v_pk_add_f32 v[50:51], v[20:21], v[28:29]
	v_pk_add_f32 v[20:21], v[20:21], v[28:29] neg_lo:[0,1] neg_hi:[0,1]
	s_nop 0
	v_xor_b32_e32 v29, 0x80000000, v20
	v_mov_b32_e32 v28, v21
	v_pk_add_f32 v[20:21], v[96:97], v[42:43]
	v_pk_add_f32 v[42:43], v[96:97], v[42:43] neg_lo:[0,1] neg_hi:[0,1]
	s_nop 0
	v_pk_mul_f32 v[96:97], v[10:11], v[42:43] op_sel:[0,1] op_sel_hi:[0,0] neg_lo:[1,1] neg_hi:[1,0]
	v_pk_fma_f32 v[42:43], v[10:11], v[42:43], v[96:97] op_sel_hi:[0,1,1] neg_lo:[1,0,0] neg_hi:[1,0,0]
	v_pk_add_f32 v[96:97], v[24:25], v[50:51]
	v_pk_add_f32 v[24:25], v[24:25], v[50:51] neg_lo:[0,1] neg_hi:[0,1]
	v_pk_add_f32 v[50:51], v[34:35], v[20:21]
	v_pk_add_f32 v[20:21], v[34:35], v[20:21] neg_lo:[0,1] neg_hi:[0,1]
	v_pk_add_f32 v[102:103], v[96:97], v[50:51]
	v_xor_b32_e32 v101, 0x80000000, v20
	v_mov_b32_e32 v100, v21
	v_pk_add_f32 v[34:35], v[96:97], v[50:51] neg_lo:[0,1] neg_hi:[0,1]
	v_pk_add_f32 v[20:21], v[98:99], v[28:29]
	v_pk_add_f32 v[96:97], v[98:99], v[28:29] neg_lo:[0,1] neg_hi:[0,1]
	v_pk_add_f32 v[28:29], v[76:77], v[42:43]
	v_pk_add_f32 v[42:43], v[76:77], v[42:43] neg_lo:[0,1] neg_hi:[0,1]
	v_pk_add_f32 v[98:99], v[20:21], v[28:29]
	v_xor_b32_e32 v77, 0x80000000, v42
	v_mov_b32_e32 v76, v43
	v_pk_add_f32 v[28:29], v[20:21], v[28:29] neg_lo:[0,1] neg_hi:[0,1]
	v_pk_add_f32 v[42:43], v[96:97], v[76:77]
	v_pk_add_f32 v[20:21], v[96:97], v[76:77] neg_lo:[0,1] neg_hi:[0,1]
	v_pk_add_f32 v[76:77], v[40:41], v[92:93]
	v_pk_add_f32 v[92:93], v[40:41], v[92:93] neg_lo:[0,1] neg_hi:[0,1]
	v_pk_add_f32 v[40:41], v[44:45], v[78:79]
	v_pk_add_f32 v[44:45], v[44:45], v[78:79] neg_lo:[0,1] neg_hi:[0,1]
	v_pk_add_f32 v[50:51], v[24:25], v[100:101]
	v_pk_mul_f32 v[78:79], v[36:37], v[44:45] op_sel:[0,1] op_sel_hi:[0,0] neg_lo:[1,1] neg_hi:[1,0]
	v_pk_fma_f32 v[44:45], v[32:33], v[44:45], v[78:79] op_sel_hi:[0,1,1]
	v_pk_add_f32 v[78:79], v[48:49], v[80:81]
	v_pk_add_f32 v[48:49], v[48:49], v[80:81] neg_lo:[0,1] neg_hi:[0,1]
	v_pk_add_f32 v[24:25], v[24:25], v[100:101] neg_lo:[0,1] neg_hi:[0,1]
	v_pk_mul_f32 v[80:81], v[10:11], v[48:49] op_sel:[0,1] op_sel_hi:[0,0] neg_lo:[1,1] neg_hi:[1,0]
	v_pk_fma_f32 v[80:81], v[10:11], v[48:49], v[80:81] op_sel_hi:[0,1,1]
	v_pk_add_f32 v[48:49], v[52:53], v[82:83]
	v_pk_add_f32 v[52:53], v[52:53], v[82:83] neg_lo:[0,1] neg_hi:[0,1]
	s_nop 0
	v_pk_mul_f32 v[82:83], v[32:33], v[52:53] op_sel:[0,1] op_sel_hi:[0,0] neg_lo:[1,1] neg_hi:[1,0]
	v_pk_fma_f32 v[52:53], v[36:37], v[52:53], v[82:83] op_sel_hi:[0,1,1]
	v_pk_add_f32 v[82:83], v[54:55], v[84:85]
	v_pk_add_f32 v[54:55], v[54:55], v[84:85] neg_lo:[0,1] neg_hi:[0,1]
	s_nop 0
	v_xor_b32_e32 v85, 0x80000000, v54
	v_mov_b32_e32 v84, v55
	v_pk_add_f32 v[54:55], v[56:57], v[86:87]
	v_pk_add_f32 v[56:57], v[56:57], v[86:87] neg_lo:[0,1] neg_hi:[0,1]
	s_nop 0
	v_pk_mul_f32 v[86:87], v[32:33], v[56:57] op_sel:[0,1] op_sel_hi:[0,0] neg_lo:[1,1] neg_hi:[1,0]
	v_pk_fma_f32 v[56:57], v[36:37], v[56:57], v[86:87] op_sel_hi:[0,1,1] neg_lo:[1,0,0] neg_hi:[1,0,0]
	v_pk_add_f32 v[86:87], v[58:59], v[88:89]
	v_pk_add_f32 v[58:59], v[58:59], v[88:89] neg_lo:[0,1] neg_hi:[0,1]
	s_nop 0
	v_pk_mul_f32 v[88:89], v[10:11], v[58:59] op_sel:[0,1] op_sel_hi:[0,0] neg_lo:[1,1] neg_hi:[1,0]
	v_pk_fma_f32 v[58:59], v[10:11], v[58:59], v[88:89] op_sel_hi:[0,1,1] neg_lo:[1,0,0] neg_hi:[1,0,0]
	v_pk_add_f32 v[88:89], v[60:61], v[90:91]
	v_pk_add_f32 v[60:61], v[60:61], v[90:91] neg_lo:[0,1] neg_hi:[0,1]
	s_nop 0
	v_pk_mul_f32 v[36:37], v[36:37], v[60:61] op_sel:[0,1] op_sel_hi:[0,0] neg_lo:[1,1] neg_hi:[1,0]
	v_pk_fma_f32 v[36:37], v[32:33], v[60:61], v[36:37] op_sel_hi:[0,1,1] neg_lo:[1,0,0] neg_hi:[1,0,0]
	v_pk_add_f32 v[32:33], v[76:77], v[82:83]
	v_pk_add_f32 v[60:61], v[76:77], v[82:83] neg_lo:[0,1] neg_hi:[0,1]
	v_pk_add_f32 v[76:77], v[54:55], v[40:41]
	v_pk_add_f32 v[40:41], v[40:41], v[54:55] neg_lo:[0,1] neg_hi:[0,1]
	s_nop 0
	v_pk_mul_f32 v[54:55], v[10:11], v[40:41] op_sel:[0,1] op_sel_hi:[0,0] neg_lo:[1,1] neg_hi:[1,0]
	v_pk_fma_f32 v[54:55], v[10:11], v[40:41], v[54:55] op_sel_hi:[0,1,1]
	v_pk_add_f32 v[40:41], v[78:79], v[86:87]
	v_pk_add_f32 v[78:79], v[78:79], v[86:87] neg_lo:[0,1] neg_hi:[0,1]
	s_nop 0
	v_xor_b32_e32 v83, 0x80000000, v78
	v_mov_b32_e32 v82, v79
	v_pk_add_f32 v[78:79], v[48:49], v[88:89]
	v_pk_add_f32 v[48:49], v[48:49], v[88:89] neg_lo:[0,1] neg_hi:[0,1]
	v_pk_add_f32 v[88:89], v[76:77], v[78:79]
	v_pk_mul_f32 v[86:87], v[10:11], v[48:49] op_sel:[0,1] op_sel_hi:[0,0] neg_lo:[1,1] neg_hi:[1,0]
	v_pk_fma_f32 v[48:49], v[10:11], v[48:49], v[86:87] op_sel_hi:[0,1,1] neg_lo:[1,0,0] neg_hi:[1,0,0]
	v_pk_add_f32 v[86:87], v[32:33], v[40:41]
	v_pk_add_f32 v[32:33], v[32:33], v[40:41] neg_lo:[0,1] neg_hi:[0,1]
	v_pk_add_f32 v[40:41], v[76:77], v[78:79] neg_lo:[0,1] neg_hi:[0,1]
	v_pk_add_f32 v[78:79], v[86:87], v[88:89] neg_lo:[0,1] neg_hi:[0,1]
	v_pk_add_f32 v[90:91], v[32:33], v[40:41] op_sel:[0,1] op_sel_hi:[1,0] neg_hi:[0,1]
	v_pk_add_f32 v[40:41], v[32:33], v[40:41] op_sel:[0,1] op_sel_hi:[1,0] neg_lo:[0,1]
	v_pk_add_f32 v[76:77], v[54:55], v[48:49]
	v_pk_add_f32 v[48:49], v[54:55], v[48:49] neg_lo:[0,1] neg_hi:[0,1]
	v_pk_add_f32 v[32:33], v[60:61], v[82:83]
	v_pk_add_f32 v[60:61], v[60:61], v[82:83] neg_lo:[0,1] neg_hi:[0,1]
	v_xor_b32_e32 v55, 0x80000000, v48
	v_mov_b32_e32 v54, v49
	v_pk_add_f32 v[82:83], v[32:33], v[76:77]
	v_pk_add_f32 v[48:49], v[32:33], v[76:77] neg_lo:[0,1] neg_hi:[0,1]
	v_pk_add_f32 v[76:77], v[60:61], v[54:55]
	v_pk_add_f32 v[32:33], v[60:61], v[54:55] neg_lo:[0,1] neg_hi:[0,1]
	v_pk_add_f32 v[54:55], v[92:93], v[84:85]
	v_pk_add_f32 v[60:61], v[92:93], v[84:85] neg_lo:[0,1] neg_hi:[0,1]
	v_pk_add_f32 v[84:85], v[56:57], v[44:45]
	v_pk_add_f32 v[44:45], v[44:45], v[56:57] neg_lo:[0,1] neg_hi:[0,1]
	v_pk_add_f32 v[86:87], v[86:87], v[88:89]
	v_pk_mul_f32 v[56:57], v[10:11], v[44:45] op_sel:[0,1] op_sel_hi:[0,0] neg_lo:[1,1] neg_hi:[1,0]
	v_pk_fma_f32 v[56:57], v[10:11], v[44:45], v[56:57] op_sel_hi:[0,1,1]
	v_pk_add_f32 v[44:45], v[80:81], v[58:59]
	v_pk_add_f32 v[58:59], v[80:81], v[58:59] neg_lo:[0,1] neg_hi:[0,1]
	s_nop 0
	v_xor_b32_e32 v81, 0x80000000, v58
	v_mov_b32_e32 v80, v59
	v_pk_add_f32 v[58:59], v[52:53], v[36:37]
	v_pk_add_f32 v[36:37], v[52:53], v[36:37] neg_lo:[0,1] neg_hi:[0,1]
	s_nop 0
	v_pk_mul_f32 v[52:53], v[10:11], v[36:37] op_sel:[0,1] op_sel_hi:[0,0] neg_lo:[1,1] neg_hi:[1,0]
	v_pk_fma_f32 v[36:37], v[10:11], v[36:37], v[52:53] op_sel_hi:[0,1,1] neg_lo:[1,0,0] neg_hi:[1,0,0]
	v_pk_add_f32 v[52:53], v[54:55], v[44:45]
	v_pk_add_f32 v[44:45], v[54:55], v[44:45] neg_lo:[0,1] neg_hi:[0,1]
	v_pk_add_f32 v[54:55], v[84:85], v[58:59]
	v_pk_add_f32 v[58:59], v[84:85], v[58:59] neg_lo:[0,1] neg_hi:[0,1]
	s_nop 0
	v_xor_b32_e32 v85, 0x80000000, v58
	v_mov_b32_e32 v84, v59
	v_pk_add_f32 v[58:59], v[52:53], v[54:55]
	v_pk_add_f32 v[52:53], v[52:53], v[54:55] neg_lo:[0,1] neg_hi:[0,1]
	v_pk_add_f32 v[54:55], v[44:45], v[84:85]
	v_pk_add_f32 v[44:45], v[44:45], v[84:85] neg_lo:[0,1] neg_hi:[0,1]
	v_pk_add_f32 v[84:85], v[60:61], v[80:81]
	v_pk_add_f32 v[60:61], v[60:61], v[80:81] neg_lo:[0,1] neg_hi:[0,1]
	v_pk_add_f32 v[80:81], v[56:57], v[36:37]
	v_pk_add_f32 v[36:37], v[56:57], v[36:37] neg_lo:[0,1] neg_hi:[0,1]
	v_pk_add_f32 v[92:93], v[84:85], v[80:81]
	v_pk_add_f32 v[80:81], v[84:85], v[80:81] neg_lo:[0,1] neg_hi:[0,1]
	v_pk_add_f32 v[84:85], v[60:61], v[36:37] op_sel:[0,1] op_sel_hi:[1,0] neg_hi:[0,1]
	v_pk_add_f32 v[36:37], v[60:61], v[36:37] op_sel:[0,1] op_sel_hi:[1,0] neg_lo:[0,1]
	v_pk_fma_f32 v[60:61], v[16:17], s[92:93], v[16:17] op_sel:[1,0,0] op_sel_hi:[0,1,1]
	v_pk_mul_f32 v[56:57], v[94:95], s[14:15] op_sel:[1,0] neg_lo:[1,0]
	v_pk_mul_f32 v[88:89], v[60:61], v[86:87] op_sel:[1,1] op_sel_hi:[0,1] neg_lo:[0,1]
	v_pk_fma_f32 v[56:57], v[94:95], s[42:43], v[56:57] op_sel_hi:[0,1,1]
	v_pk_fma_f32 v[86:87], v[60:61], v[86:87], v[88:89] op_sel_hi:[1,0,1]
	ds_write2_b64 v75, v[56:57], v[86:87] offset1:16
	v_pk_mul_f32 v[56:57], v[16:17], v[60:61] op_sel:[1,1] op_sel_hi:[0,1] neg_lo:[0,1]
	v_pk_fma_f32 v[56:57], v[16:17], v[60:61], v[56:57] op_sel_hi:[1,0,1]
	s_nop 0
	v_pk_mul_f32 v[60:61], v[56:57], v[102:103] op_sel:[1,1] op_sel_hi:[0,1] neg_lo:[0,1]
	v_pk_mul_f32 v[86:87], v[16:17], v[56:57] op_sel:[1,1] op_sel_hi:[0,1] neg_lo:[0,1]
	v_pk_fma_f32 v[60:61], v[56:57], v[102:103], v[60:61] op_sel_hi:[1,0,1]
	v_pk_fma_f32 v[56:57], v[16:17], v[56:57], v[86:87] op_sel_hi:[1,0,1]
	s_nop 0
	v_pk_mul_f32 v[86:87], v[56:57], v[58:59] op_sel:[1,1] op_sel_hi:[0,1] neg_lo:[0,1]
	v_pk_fma_f32 v[58:59], v[56:57], v[58:59], v[86:87] op_sel_hi:[1,0,1]
	ds_write2_b64 v74, v[60:61], v[58:59] offset0:32 offset1:48
	v_pk_mul_f32 v[58:59], v[16:17], v[56:57] op_sel:[1,1] op_sel_hi:[0,1] neg_lo:[0,1]
	v_pk_fma_f32 v[56:57], v[16:17], v[56:57], v[58:59] op_sel_hi:[1,0,1]
	s_nop 0
	v_pk_mul_f32 v[58:59], v[56:57], v[104:105] op_sel:[1,1] op_sel_hi:[0,1] neg_lo:[0,1]
	v_pk_mul_f32 v[60:61], v[16:17], v[56:57] op_sel:[1,1] op_sel_hi:[0,1] neg_lo:[0,1]
	v_pk_fma_f32 v[58:59], v[56:57], v[104:105], v[58:59] op_sel_hi:[1,0,1]
	v_pk_fma_f32 v[56:57], v[16:17], v[56:57], v[60:61] op_sel_hi:[1,0,1]
	s_nop 0
	v_pk_mul_f32 v[60:61], v[56:57], v[82:83] op_sel:[1,1] op_sel_hi:[0,1] neg_lo:[0,1]
	v_pk_fma_f32 v[60:61], v[56:57], v[82:83], v[60:61] op_sel_hi:[1,0,1]
	ds_write2_b64 v73, v[58:59], v[60:61] offset0:64 offset1:80
	v_pk_mul_f32 v[58:59], v[16:17], v[56:57] op_sel:[1,1] op_sel_hi:[0,1] neg_lo:[0,1]
	v_pk_fma_f32 v[56:57], v[16:17], v[56:57], v[58:59] op_sel_hi:[1,0,1]
	s_nop 0
	v_pk_mul_f32 v[58:59], v[56:57], v[98:99] op_sel:[1,1] op_sel_hi:[0,1] neg_lo:[0,1]
	v_pk_mul_f32 v[60:61], v[16:17], v[56:57] op_sel:[1,1] op_sel_hi:[0,1] neg_lo:[0,1]
	v_pk_fma_f32 v[58:59], v[56:57], v[98:99], v[58:59] op_sel_hi:[1,0,1]
	v_pk_fma_f32 v[56:57], v[16:17], v[56:57], v[60:61] op_sel_hi:[1,0,1]
	s_nop 0
	v_pk_mul_f32 v[60:61], v[56:57], v[92:93] op_sel:[1,1] op_sel_hi:[0,1] neg_lo:[0,1]
	v_pk_fma_f32 v[60:61], v[56:57], v[92:93], v[60:61] op_sel_hi:[1,0,1]
	ds_write2_b64 v72, v[58:59], v[60:61] offset0:96 offset1:112
	v_pk_mul_f32 v[58:59], v[16:17], v[56:57] op_sel:[1,1] op_sel_hi:[0,1] neg_lo:[0,1]
	v_pk_fma_f32 v[56:57], v[16:17], v[56:57], v[58:59] op_sel_hi:[1,0,1]
	s_nop 0
	v_pk_mul_f32 v[58:59], v[56:57], v[46:47] op_sel:[1,1] op_sel_hi:[0,1] neg_lo:[0,1]
	v_pk_fma_f32 v[46:47], v[56:57], v[46:47], v[58:59] op_sel_hi:[1,0,1]
	v_pk_mul_f32 v[58:59], v[16:17], v[56:57] op_sel:[1,1] op_sel_hi:[0,1] neg_lo:[0,1]
	v_pk_fma_f32 v[56:57], v[16:17], v[56:57], v[58:59] op_sel_hi:[1,0,1]
	s_nop 0
	v_pk_mul_f32 v[58:59], v[56:57], v[90:91] op_sel:[1,1] op_sel_hi:[0,1] neg_lo:[0,1]
	v_pk_fma_f32 v[58:59], v[56:57], v[90:91], v[58:59] op_sel_hi:[1,0,1]
	ds_write2_b64 v71, v[46:47], v[58:59] offset0:128 offset1:144
	v_pk_mul_f32 v[46:47], v[16:17], v[56:57] op_sel:[1,1] op_sel_hi:[0,1] neg_lo:[0,1]
	v_pk_fma_f32 v[46:47], v[16:17], v[56:57], v[46:47] op_sel_hi:[1,0,1]
	s_nop 0
	v_pk_mul_f32 v[56:57], v[46:47], v[50:51] op_sel:[1,1] op_sel_hi:[0,1] neg_lo:[0,1]
	v_pk_fma_f32 v[50:51], v[46:47], v[50:51], v[56:57] op_sel_hi:[1,0,1]
	v_pk_mul_f32 v[56:57], v[16:17], v[46:47] op_sel:[1,1] op_sel_hi:[0,1] neg_lo:[0,1]
	v_pk_fma_f32 v[46:47], v[16:17], v[46:47], v[56:57] op_sel_hi:[1,0,1]
	s_nop 0
	v_pk_mul_f32 v[56:57], v[46:47], v[54:55] op_sel:[1,1] op_sel_hi:[0,1] neg_lo:[0,1]
	v_pk_fma_f32 v[54:55], v[46:47], v[54:55], v[56:57] op_sel_hi:[1,0,1]
	ds_write2_b64 v70, v[50:51], v[54:55] offset0:160 offset1:176
	v_pk_mul_f32 v[50:51], v[16:17], v[46:47] op_sel:[1,1] op_sel_hi:[0,1] neg_lo:[0,1]
	v_pk_fma_f32 v[46:47], v[16:17], v[46:47], v[50:51] op_sel_hi:[1,0,1]
	s_nop 0
	v_pk_mul_f32 v[50:51], v[38:39], v[46:47] op_sel:[1,1] op_sel_hi:[1,0] neg_lo:[1,0]
	s_nop 0
	v_pk_fma_f32 v[38:39], v[38:39], v[46:47], v[50:51] op_sel_hi:[0,1,1]
	v_pk_mul_f32 v[50:51], v[16:17], v[46:47] op_sel:[1,1] op_sel_hi:[0,1] neg_lo:[0,1]
	v_pk_fma_f32 v[46:47], v[16:17], v[46:47], v[50:51] op_sel_hi:[1,0,1]
	s_nop 0
	v_pk_mul_f32 v[50:51], v[46:47], v[76:77] op_sel:[1,1] op_sel_hi:[0,1] neg_lo:[0,1]
	v_pk_fma_f32 v[50:51], v[46:47], v[76:77], v[50:51] op_sel_hi:[1,0,1]
	ds_write2_b64 v69, v[38:39], v[50:51] offset0:192 offset1:208
	v_pk_mul_f32 v[38:39], v[16:17], v[46:47] op_sel:[1,1] op_sel_hi:[0,1] neg_lo:[0,1]
	v_pk_fma_f32 v[38:39], v[16:17], v[46:47], v[38:39] op_sel_hi:[1,0,1]
	s_nop 0
	v_pk_mul_f32 v[46:47], v[42:43], v[38:39] op_sel:[1,1] op_sel_hi:[1,0] neg_lo:[1,0]
	s_nop 0
	v_pk_fma_f32 v[42:43], v[42:43], v[38:39], v[46:47] op_sel_hi:[0,1,1]
	v_pk_mul_f32 v[46:47], v[16:17], v[38:39] op_sel:[1,1] op_sel_hi:[0,1] neg_lo:[0,1]
	v_pk_fma_f32 v[38:39], v[16:17], v[38:39], v[46:47] op_sel_hi:[1,0,1]
	s_nop 0
	v_pk_mul_f32 v[46:47], v[38:39], v[84:85] op_sel:[1,1] op_sel_hi:[0,1] neg_lo:[0,1]
	v_pk_fma_f32 v[46:47], v[38:39], v[84:85], v[46:47] op_sel_hi:[1,0,1]
	ds_write2_b64 v68, v[42:43], v[46:47] offset0:224 offset1:240
	v_pk_mul_f32 v[42:43], v[16:17], v[38:39] op_sel:[1,1] op_sel_hi:[0,1] neg_lo:[0,1]
	v_pk_fma_f32 v[38:39], v[16:17], v[38:39], v[42:43] op_sel_hi:[1,0,1]
	s_nop 0
	v_pk_mul_f32 v[42:43], v[30:31], v[38:39] op_sel:[1,1] op_sel_hi:[1,0] neg_lo:[1,0]
	s_nop 0
	v_pk_fma_f32 v[30:31], v[30:31], v[38:39], v[42:43] op_sel_hi:[0,1,1]
	v_pk_mul_f32 v[42:43], v[16:17], v[38:39] op_sel:[1,1] op_sel_hi:[0,1] neg_lo:[0,1]
	v_pk_fma_f32 v[38:39], v[16:17], v[38:39], v[42:43] op_sel_hi:[1,0,1]
	s_nop 0
	v_pk_mul_f32 v[42:43], v[78:79], v[38:39] op_sel:[1,1] op_sel_hi:[1,0] neg_lo:[1,0]
	s_nop 0
	v_pk_fma_f32 v[42:43], v[78:79], v[38:39], v[42:43] op_sel_hi:[0,1,1]
	ds_write2_b64 v67, v[30:31], v[42:43] offset1:16
	v_pk_mul_f32 v[30:31], v[16:17], v[38:39] op_sel:[1,1] op_sel_hi:[0,1] neg_lo:[0,1]
	v_pk_fma_f32 v[30:31], v[16:17], v[38:39], v[30:31] op_sel_hi:[1,0,1]
	s_nop 0
	v_pk_mul_f32 v[38:39], v[34:35], v[30:31] op_sel:[1,1] op_sel_hi:[1,0] neg_lo:[1,0]
	s_nop 0
	v_pk_fma_f32 v[34:35], v[34:35], v[30:31], v[38:39] op_sel_hi:[0,1,1]
	v_pk_mul_f32 v[38:39], v[16:17], v[30:31] op_sel:[1,1] op_sel_hi:[0,1] neg_lo:[0,1]
	v_pk_fma_f32 v[30:31], v[16:17], v[30:31], v[38:39] op_sel_hi:[1,0,1]
	s_nop 0
	v_pk_mul_f32 v[38:39], v[52:53], v[30:31] op_sel:[1,1] op_sel_hi:[1,0] neg_lo:[1,0]
	s_nop 0
	v_pk_fma_f32 v[38:39], v[52:53], v[30:31], v[38:39] op_sel_hi:[0,1,1]
	ds_write2_b64 v66, v[34:35], v[38:39] offset0:32 offset1:48
	v_pk_mul_f32 v[34:35], v[16:17], v[30:31] op_sel:[1,1] op_sel_hi:[0,1] neg_lo:[0,1]
	v_pk_fma_f32 v[30:31], v[16:17], v[30:31], v[34:35] op_sel_hi:[1,0,1]
	s_nop 0
	v_pk_mul_f32 v[34:35], v[26:27], v[30:31] op_sel:[1,1] op_sel_hi:[1,0] neg_lo:[1,0]
	s_nop 0
	v_pk_fma_f32 v[26:27], v[26:27], v[30:31], v[34:35] op_sel_hi:[0,1,1]
	v_pk_mul_f32 v[34:35], v[16:17], v[30:31] op_sel:[1,1] op_sel_hi:[0,1] neg_lo:[0,1]
	v_pk_fma_f32 v[30:31], v[16:17], v[30:31], v[34:35] op_sel_hi:[1,0,1]
	s_nop 0
	v_pk_mul_f32 v[34:35], v[48:49], v[30:31] op_sel:[1,1] op_sel_hi:[1,0] neg_lo:[1,0]
	s_nop 0
	v_pk_fma_f32 v[34:35], v[48:49], v[30:31], v[34:35] op_sel_hi:[0,1,1]
	ds_write2_b64 v65, v[26:27], v[34:35] offset0:64 offset1:80
	v_pk_mul_f32 v[26:27], v[16:17], v[30:31] op_sel:[1,1] op_sel_hi:[0,1] neg_lo:[0,1]
	v_pk_fma_f32 v[26:27], v[16:17], v[30:31], v[26:27] op_sel_hi:[1,0,1]
	s_nop 0
	v_pk_mul_f32 v[30:31], v[28:29], v[26:27] op_sel:[1,1] op_sel_hi:[1,0] neg_lo:[1,0]
	s_nop 0
	v_pk_fma_f32 v[28:29], v[28:29], v[26:27], v[30:31] op_sel_hi:[0,1,1]
	v_pk_mul_f32 v[30:31], v[16:17], v[26:27] op_sel:[1,1] op_sel_hi:[0,1] neg_lo:[0,1]
	v_pk_fma_f32 v[26:27], v[16:17], v[26:27], v[30:31] op_sel_hi:[1,0,1]
	s_nop 0
	v_pk_mul_f32 v[30:31], v[80:81], v[26:27] op_sel:[1,1] op_sel_hi:[1,0] neg_lo:[1,0]
	s_nop 0
	v_pk_fma_f32 v[30:31], v[80:81], v[26:27], v[30:31] op_sel_hi:[0,1,1]
	ds_write2_b64 v64, v[28:29], v[30:31] offset0:96 offset1:112
	v_pk_mul_f32 v[28:29], v[16:17], v[26:27] op_sel:[1,1] op_sel_hi:[0,1] neg_lo:[0,1]
	v_pk_fma_f32 v[26:27], v[16:17], v[26:27], v[28:29] op_sel_hi:[1,0,1]
	s_nop 0
	v_pk_mul_f32 v[28:29], v[22:23], v[26:27] op_sel:[1,1] op_sel_hi:[1,0] neg_lo:[1,0]
	s_nop 0
	v_pk_fma_f32 v[22:23], v[22:23], v[26:27], v[28:29] op_sel_hi:[0,1,1]
	v_pk_mul_f32 v[28:29], v[16:17], v[26:27] op_sel:[1,1] op_sel_hi:[0,1] neg_lo:[0,1]
	v_pk_fma_f32 v[26:27], v[16:17], v[26:27], v[28:29] op_sel_hi:[1,0,1]
	s_nop 0
	v_pk_mul_f32 v[28:29], v[40:41], v[26:27] op_sel:[1,1] op_sel_hi:[1,0] neg_lo:[1,0]
	s_nop 0
	v_pk_fma_f32 v[28:29], v[40:41], v[26:27], v[28:29] op_sel_hi:[0,1,1]
	ds_write2_b64 v63, v[22:23], v[28:29] offset0:128 offset1:144
	v_pk_mul_f32 v[22:23], v[16:17], v[26:27] op_sel:[1,1] op_sel_hi:[0,1] neg_lo:[0,1]
	v_pk_fma_f32 v[22:23], v[16:17], v[26:27], v[22:23] op_sel_hi:[1,0,1]
	s_nop 0
	v_pk_mul_f32 v[26:27], v[24:25], v[22:23] op_sel:[1,1] op_sel_hi:[1,0] neg_lo:[1,0]
	s_nop 0
	v_pk_fma_f32 v[24:25], v[24:25], v[22:23], v[26:27] op_sel_hi:[0,1,1]
	v_pk_mul_f32 v[26:27], v[16:17], v[22:23] op_sel:[1,1] op_sel_hi:[0,1] neg_lo:[0,1]
	v_pk_fma_f32 v[22:23], v[16:17], v[22:23], v[26:27] op_sel_hi:[1,0,1]
	s_nop 0
	v_pk_mul_f32 v[26:27], v[44:45], v[22:23] op_sel:[1,1] op_sel_hi:[1,0] neg_lo:[1,0]
	s_nop 0
	v_pk_fma_f32 v[26:27], v[44:45], v[22:23], v[26:27] op_sel_hi:[0,1,1]
	ds_write2_b64 v62, v[24:25], v[26:27] offset0:160 offset1:176
	v_pk_mul_f32 v[24:25], v[16:17], v[22:23] op_sel:[1,1] op_sel_hi:[0,1] neg_lo:[0,1]
	v_pk_fma_f32 v[22:23], v[16:17], v[22:23], v[24:25] op_sel_hi:[1,0,1]
	s_nop 0
	v_pk_mul_f32 v[24:25], v[18:19], v[22:23] op_sel:[1,1] op_sel_hi:[1,0] neg_lo:[1,0]
	s_nop 0
	v_pk_fma_f32 v[18:19], v[18:19], v[22:23], v[24:25] op_sel_hi:[0,1,1]
	v_pk_mul_f32 v[24:25], v[16:17], v[22:23] op_sel:[1,1] op_sel_hi:[0,1] neg_lo:[0,1]
	v_pk_fma_f32 v[22:23], v[16:17], v[22:23], v[24:25] op_sel_hi:[1,0,1]
	s_nop 0
	v_pk_mul_f32 v[24:25], v[32:33], v[22:23] op_sel:[1,1] op_sel_hi:[1,0] neg_lo:[1,0]
	s_nop 0
	v_pk_fma_f32 v[24:25], v[32:33], v[22:23], v[24:25] op_sel_hi:[0,1,1]
	ds_write2_b64 v15, v[18:19], v[24:25] offset0:192 offset1:208
	v_pk_mul_f32 v[18:19], v[16:17], v[22:23] op_sel:[1,1] op_sel_hi:[0,1] neg_lo:[0,1]
	v_pk_fma_f32 v[18:19], v[16:17], v[22:23], v[18:19] op_sel_hi:[1,0,1]
	s_nop 0
	v_pk_mul_f32 v[22:23], v[20:21], v[18:19] op_sel:[1,1] op_sel_hi:[1,0] neg_lo:[1,0]
	s_nop 0
	v_pk_fma_f32 v[20:21], v[20:21], v[18:19], v[22:23] op_sel_hi:[0,1,1]
	v_pk_mul_f32 v[22:23], v[16:17], v[18:19] op_sel:[1,1] op_sel_hi:[0,1] neg_lo:[0,1]
	v_pk_fma_f32 v[16:17], v[16:17], v[18:19], v[22:23] op_sel_hi:[1,0,1]
	s_nop 0
	v_pk_mul_f32 v[18:19], v[36:37], v[16:17] op_sel:[1,1] op_sel_hi:[1,0] neg_lo:[1,0]
	s_nop 0
	v_pk_fma_f32 v[16:17], v[36:37], v[16:17], v[18:19] op_sel_hi:[0,1,1]
	ds_write2_b64 v13, v[20:21], v[16:17] offset0:224 offset1:240
	v_mov_b32_e32 v16, v1
	v_mov_b32_e32 v10, v178
	v_mov_b32_e32 v17, v177
	s_waitcnt lgkmcnt(0)
	s_barrier
	v_lshlrev_b32_e32 v190, 3, v16
	v_add_u32_e32 v190, 0x1000, v190
	global_load_dwordx2 v[196:197], v190, s[48:49] offset:-4096
	global_load_dwordx2 v[198:199], v190, s[48:49]
	v_add_u32_e32 v190, 0x2000, v190
	global_load_dwordx2 v[200:201], v190, s[48:49] offset:-4096
	global_load_dwordx2 v[202:203], v190, s[48:49]
	v_add_u32_e32 v190, 0x2000, v190
	global_load_dwordx2 v[204:205], v190, s[48:49] offset:-4096
	global_load_dwordx2 v[206:207], v190, s[48:49]
	v_add_u32_e32 v190, 0x2000, v190
	global_load_dwordx2 v[208:209], v190, s[48:49] offset:-4096
	global_load_dwordx2 v[210:211], v190, s[48:49]
	v_add_u32_e32 v190, 0x2000, v190
	global_load_dwordx2 v[212:213], v190, s[48:49] offset:-4096
	global_load_dwordx2 v[214:215], v190, s[48:49]
	v_add_u32_e32 v190, 0x2000, v190
	global_load_dwordx2 v[216:217], v190, s[48:49] offset:-4096
	global_load_dwordx2 v[218:219], v190, s[48:49]
	v_add_u32_e32 v190, 0x2000, v190
	global_load_dwordx2 v[220:221], v190, s[48:49] offset:-4096
	global_load_dwordx2 v[222:223], v190, s[48:49]
	v_add_u32_e32 v190, 0x2000, v190
	global_load_dwordx2 v[224:225], v190, s[48:49] offset:-4096
	global_load_dwordx2 v[226:227], v190, s[48:49]
	v_mov_b32_e32 v50, v166
	v_lshlrev_b32_e32 v13, 3, v17
	v_lshlrev_b32_e32 v48, 3, v10
	v_add3_u32 v10, 0, v13, v48
	v_xor_b32_e32 v13, 1, v17
	v_xor_b32_e32 v34, 8, v17
	v_xor_b32_e32 v36, 9, v17
	v_lshlrev_b32_e32 v13, 3, v13
	v_xor_b32_e32 v15, 2, v17
	v_xor_b32_e32 v24, 3, v17
	v_xor_b32_e32 v26, 4, v17
	v_xor_b32_e32 v28, 5, v17
	v_xor_b32_e32 v30, 6, v17
	v_xor_b32_e32 v32, 7, v17
	v_lshlrev_b32_e32 v34, 3, v34
	v_lshlrev_b32_e32 v36, 3, v36
	v_xor_b32_e32 v38, 10, v17
	v_xor_b32_e32 v40, 11, v17
	v_xor_b32_e32 v42, 12, v17
	v_xor_b32_e32 v44, 13, v17
	v_xor_b32_e32 v46, 14, v17
	v_xor_b32_e32 v17, 15, v17
	v_add3_u32 v13, 0, v13, v48
	v_lshlrev_b32_e32 v15, 3, v15
	v_lshlrev_b32_e32 v24, 3, v24
	v_lshlrev_b32_e32 v26, 3, v26
	v_lshlrev_b32_e32 v28, 3, v28
	v_lshlrev_b32_e32 v30, 3, v30
	v_lshlrev_b32_e32 v32, 3, v32
	v_add3_u32 v57, 0, v34, v48
	v_add3_u32 v58, 0, v36, v48
	v_lshlrev_b32_e32 v38, 3, v38
	v_lshlrev_b32_e32 v40, 3, v40
	v_lshlrev_b32_e32 v42, 3, v42
	v_lshlrev_b32_e32 v44, 3, v44
	v_lshlrev_b32_e32 v46, 3, v46
	v_lshlrev_b32_e32 v17, 3, v17
	ds_read_b64 v[18:19], v10
	ds_read_b64 v[20:21], v13
	v_add3_u32 v15, 0, v15, v48
	v_add3_u32 v52, 0, v24, v48
	v_add3_u32 v53, 0, v26, v48
	v_add3_u32 v54, 0, v28, v48
	v_add3_u32 v55, 0, v30, v48
	v_add3_u32 v56, 0, v32, v48
	ds_read_b64 v[34:35], v57
	ds_read_b64 v[36:37], v58
	v_add3_u32 v59, 0, v38, v48
	v_add3_u32 v60, 0, v40, v48
	v_add3_u32 v61, 0, v42, v48
	v_add3_u32 v62, 0, v44, v48
	v_add3_u32 v63, 0, v46, v48
	v_add3_u32 v64, 0, v17, v48
	ds_read_b64 v[22:23], v15
	ds_read_b64 v[24:25], v52
	ds_read_b64 v[26:27], v53
	ds_read_b64 v[28:29], v54
	ds_read_b64 v[30:31], v55
	ds_read_b64 v[32:33], v56
	ds_read_b64 v[38:39], v59
	ds_read_b64 v[40:41], v60
	ds_read_b64 v[42:43], v61
	ds_read_b64 v[44:45], v62
	ds_read_b64 v[46:47], v63
	ds_read_b64 v[48:49], v64
	s_waitcnt lgkmcnt(13)
	v_pk_add_f32 v[70:71], v[18:19], v[34:35]
	v_pk_add_f32 v[18:19], v[18:19], v[34:35] neg_lo:[0,1] neg_hi:[0,1]
	s_waitcnt lgkmcnt(12)
	v_pk_add_f32 v[34:35], v[20:21], v[36:37]
	v_pk_add_f32 v[20:21], v[20:21], v[36:37] neg_lo:[0,1] neg_hi:[0,1]
	v_mov_b32_e32 v66, v168
	v_mov_b32_e32 v68, v170
	s_nop 0
	v_pk_mul_f32 v[36:37], v[20:21], v[68:69] op_sel:[1,0] op_sel_hi:[0,0] neg_lo:[1,1] neg_hi:[0,1]
	v_pk_fma_f32 v[20:21], v[20:21], v[50:51], v[36:37] op_sel_hi:[1,0,1]
	s_waitcnt lgkmcnt(5)
	v_pk_add_f32 v[36:37], v[22:23], v[38:39]
	v_pk_add_f32 v[22:23], v[22:23], v[38:39] neg_lo:[0,1] neg_hi:[0,1]
	s_nop 0
	v_pk_mul_f32 v[38:39], v[22:23], v[66:67] op_sel:[1,0] op_sel_hi:[0,0] neg_lo:[1,1] neg_hi:[0,1]
	v_pk_fma_f32 v[22:23], v[22:23], v[66:67], v[38:39] op_sel_hi:[1,0,1]
	s_waitcnt lgkmcnt(4)
	v_pk_add_f32 v[38:39], v[24:25], v[40:41]
	v_pk_add_f32 v[24:25], v[24:25], v[40:41] neg_lo:[0,1] neg_hi:[0,1]
	s_nop 0
	v_pk_mul_f32 v[40:41], v[24:25], v[68:69] op_sel_hi:[1,0]
	s_nop 0
	v_pk_fma_f32 v[24:25], v[24:25], v[50:51], v[40:41] op_sel:[1,0,0] op_sel_hi:[0,0,1] neg_lo:[1,1,0] neg_hi:[0,1,0]
	s_waitcnt lgkmcnt(3)
	v_pk_add_f32 v[40:41], v[26:27], v[42:43]
	v_pk_add_f32 v[26:27], v[26:27], v[42:43] neg_lo:[0,1] neg_hi:[0,1]
	v_xor_b32_e32 v73, 0x80000000, v26
	v_mov_b32_e32 v72, v27
	s_waitcnt lgkmcnt(2)
	v_pk_add_f32 v[26:27], v[28:29], v[44:45]
	v_pk_add_f32 v[28:29], v[28:29], v[44:45] neg_lo:[0,1] neg_hi:[0,1]
	s_nop 0
	v_pk_mul_f32 v[42:43], v[28:29], v[68:69] op_sel_hi:[1,0] neg_lo:[0,1] neg_hi:[0,1]
	s_nop 0
	v_pk_fma_f32 v[28:29], v[28:29], v[50:51], v[42:43] op_sel:[1,0,0] op_sel_hi:[0,0,1] neg_lo:[1,1,0] neg_hi:[0,1,0]
	s_waitcnt lgkmcnt(1)
	v_pk_add_f32 v[42:43], v[30:31], v[46:47]
	v_pk_add_f32 v[30:31], v[30:31], v[46:47] neg_lo:[0,1] neg_hi:[0,1]
	s_nop 0
	v_pk_mul_f32 v[44:45], v[30:31], v[66:67] op_sel:[1,0] op_sel_hi:[0,0] neg_lo:[1,1] neg_hi:[0,1]
	s_nop 0
	v_pk_fma_f32 v[30:31], v[30:31], v[66:67], v[44:45] op_sel_hi:[1,0,1] neg_lo:[0,1,0] neg_hi:[0,1,0]
	s_waitcnt lgkmcnt(0)
	v_pk_add_f32 v[44:45], v[32:33], v[48:49]
	v_pk_add_f32 v[32:33], v[32:33], v[48:49] neg_lo:[0,1] neg_hi:[0,1]
	v_pk_add_f32 v[48:49], v[34:35], v[26:27]
	v_pk_add_f32 v[26:27], v[34:35], v[26:27] neg_lo:[0,1] neg_hi:[0,1]
	s_nop 0
	v_pk_mul_f32 v[34:35], v[26:27], v[66:67] op_sel:[1,0] op_sel_hi:[0,0] neg_lo:[1,1] neg_hi:[0,1]
	v_pk_fma_f32 v[26:27], v[26:27], v[66:67], v[34:35] op_sel_hi:[1,0,1]
	v_pk_add_f32 v[34:35], v[36:37], v[42:43]
	v_pk_add_f32 v[36:37], v[36:37], v[42:43] neg_lo:[0,1] neg_hi:[0,1]
	v_pk_mul_f32 v[46:47], v[32:33], v[68:69] op_sel:[1,0] op_sel_hi:[0,0] neg_lo:[1,1] neg_hi:[0,1]
	v_xor_b32_e32 v43, 0x80000000, v36
	v_mov_b32_e32 v42, v37
	v_pk_add_f32 v[36:37], v[38:39], v[44:45]
	v_pk_add_f32 v[38:39], v[38:39], v[44:45] neg_lo:[0,1] neg_hi:[0,1]
	v_pk_fma_f32 v[46:47], v[32:33], v[50:51], v[46:47] op_sel_hi:[1,0,1] neg_lo:[0,1,0] neg_hi:[0,1,0]
	v_pk_add_f32 v[32:33], v[70:71], v[40:41]
	v_pk_mul_f32 v[44:45], v[38:39], v[66:67] op_sel:[1,0] op_sel_hi:[0,0] neg_lo:[1,1] neg_hi:[0,1]
	v_pk_add_f32 v[40:41], v[70:71], v[40:41] neg_lo:[0,1] neg_hi:[0,1]
	v_pk_fma_f32 v[38:39], v[38:39], v[66:67], v[44:45] op_sel_hi:[1,0,1] neg_lo:[0,1,0] neg_hi:[0,1,0]
	v_pk_add_f32 v[44:45], v[32:33], v[34:35]
	v_pk_add_f32 v[32:33], v[32:33], v[34:35] neg_lo:[0,1] neg_hi:[0,1]
	v_pk_add_f32 v[34:35], v[48:49], v[36:37]
	v_pk_add_f32 v[36:37], v[48:49], v[36:37] neg_lo:[0,1] neg_hi:[0,1]
	v_pk_add_f32 v[50:51], v[44:45], v[34:35]
	v_xor_b32_e32 v49, 0x80000000, v36
	v_mov_b32_e32 v48, v37
	v_pk_add_f32 v[36:37], v[44:45], v[34:35] neg_lo:[0,1] neg_hi:[0,1]
	v_pk_add_f32 v[68:69], v[32:33], v[48:49]
	v_pk_add_f32 v[44:45], v[32:33], v[48:49] neg_lo:[0,1] neg_hi:[0,1]
	v_pk_add_f32 v[32:33], v[40:41], v[42:43]
	v_pk_add_f32 v[34:35], v[40:41], v[42:43] neg_lo:[0,1] neg_hi:[0,1]
	v_pk_add_f32 v[40:41], v[26:27], v[38:39]
	v_pk_add_f32 v[26:27], v[26:27], v[38:39] neg_lo:[0,1] neg_hi:[0,1]
	v_pk_add_f32 v[42:43], v[32:33], v[40:41] neg_lo:[0,1] neg_hi:[0,1]
	v_xor_b32_e32 v39, 0x80000000, v26
	v_mov_b32_e32 v38, v27
	v_pk_add_f32 v[26:27], v[32:33], v[40:41]
	v_pk_add_f32 v[40:41], v[20:21], v[28:29]
	v_pk_add_f32 v[20:21], v[20:21], v[28:29] neg_lo:[0,1] neg_hi:[0,1]
	v_pk_add_f32 v[32:33], v[34:35], v[38:39]
	v_pk_mul_f32 v[28:29], v[66:67], v[20:21] op_sel:[0,1] op_sel_hi:[0,0] neg_lo:[1,1] neg_hi:[1,0]
	v_pk_fma_f32 v[20:21], v[66:67], v[20:21], v[28:29] op_sel_hi:[0,1,1]
	v_pk_add_f32 v[28:29], v[22:23], v[30:31]
	v_pk_add_f32 v[22:23], v[22:23], v[30:31] neg_lo:[0,1] neg_hi:[0,1]
	v_pk_add_f32 v[38:39], v[34:35], v[38:39] neg_lo:[0,1] neg_hi:[0,1]
	v_xor_b32_e32 v31, 0x80000000, v22
	v_mov_b32_e32 v30, v23
	v_pk_add_f32 v[22:23], v[24:25], v[46:47]
	v_pk_add_f32 v[24:25], v[24:25], v[46:47] neg_lo:[0,1] neg_hi:[0,1]
	v_pk_add_f32 v[34:35], v[18:19], v[72:73]
	v_pk_mul_f32 v[46:47], v[66:67], v[24:25] op_sel:[0,1] op_sel_hi:[0,0] neg_lo:[1,1] neg_hi:[1,0]
	v_pk_fma_f32 v[24:25], v[66:67], v[24:25], v[46:47] op_sel_hi:[0,1,1] neg_lo:[1,0,0] neg_hi:[1,0,0]
	v_pk_add_f32 v[46:47], v[34:35], v[28:29]
	v_pk_add_f32 v[28:29], v[34:35], v[28:29] neg_lo:[0,1] neg_hi:[0,1]
	v_pk_add_f32 v[34:35], v[40:41], v[22:23]
	v_pk_add_f32 v[22:23], v[40:41], v[22:23] neg_lo:[0,1] neg_hi:[0,1]
	v_pk_add_f32 v[18:19], v[18:19], v[72:73] neg_lo:[0,1] neg_hi:[0,1]
	v_pk_add_f32 v[66:67], v[28:29], v[22:23] op_sel:[0,1] op_sel_hi:[1,0] neg_hi:[0,1]
	v_pk_add_f32 v[48:49], v[28:29], v[22:23] op_sel:[0,1] op_sel_hi:[1,0] neg_lo:[0,1]
	v_pk_add_f32 v[28:29], v[18:19], v[30:31]
	v_pk_add_f32 v[18:19], v[18:19], v[30:31] neg_lo:[0,1] neg_hi:[0,1]
	v_pk_add_f32 v[30:31], v[20:21], v[24:25]
	v_pk_add_f32 v[20:21], v[20:21], v[24:25] neg_lo:[0,1] neg_hi:[0,1]
	v_pk_add_f32 v[22:23], v[46:47], v[34:35]
	v_xor_b32_e32 v25, 0x80000000, v20
	v_mov_b32_e32 v24, v21
	s_waitcnt vmcnt(0)
	v_pk_add_f32 v[40:41], v[46:47], v[34:35] neg_lo:[0,1] neg_hi:[0,1]
	v_pk_add_f32 v[34:35], v[18:19], v[24:25]
	v_pk_add_f32 v[18:19], v[18:19], v[24:25] neg_lo:[0,1] neg_hi:[0,1]
	v_pk_add_f32 v[70:71], v[28:29], v[30:31]
	v_pk_add_f32 v[46:47], v[28:29], v[30:31] neg_lo:[0,1] neg_hi:[0,1]
	s_nop 0
	v_pk_mul_f32 v[24:25], v[50:51], v[196:197] op_sel:[1,1] op_sel_hi:[1,0] neg_lo:[1,0]
	s_nop 0
	v_pk_fma_f32 v[20:21], v[50:51], v[196:197], v[24:25] op_sel_hi:[0,1,1]
	s_nop 0
	v_pk_mul_f32 v[28:29], v[198:199], v[22:23] op_sel:[1,1] op_sel_hi:[0,1] neg_lo:[0,1]
	v_pk_fma_f32 v[22:23], v[198:199], v[22:23], v[28:29] op_sel_hi:[1,0,1]
	s_nop 0
	v_pk_mul_f32 v[28:29], v[26:27], v[200:201] op_sel:[1,1] op_sel_hi:[1,0] neg_lo:[1,0]
	s_nop 0
	v_pk_fma_f32 v[24:25], v[26:27], v[200:201], v[28:29] op_sel_hi:[0,1,1]
	s_nop 0
	v_pk_mul_f32 v[28:29], v[202:203], v[70:71] op_sel:[1,1] op_sel_hi:[0,1] neg_lo:[0,1]
	v_pk_fma_f32 v[26:27], v[202:203], v[70:71], v[28:29] op_sel_hi:[1,0,1]
	s_nop 0
	v_pk_mul_f32 v[30:31], v[68:69], v[204:205] op_sel:[1,1] op_sel_hi:[1,0] neg_lo:[1,0]
	s_nop 0
	v_pk_fma_f32 v[28:29], v[68:69], v[204:205], v[30:31] op_sel_hi:[0,1,1]
	v_mov_b32_e32 v68, v170
	s_nop 0
	v_pk_mul_f32 v[50:51], v[206:207], v[66:67] op_sel:[1,1] op_sel_hi:[0,1] neg_lo:[0,1]
	v_pk_fma_f32 v[30:31], v[206:207], v[66:67], v[50:51] op_sel_hi:[1,0,1]
	s_nop 0
	v_pk_mul_f32 v[66:67], v[32:33], v[208:209] op_sel:[1,1] op_sel_hi:[1,0] neg_lo:[1,0]
	s_nop 0
	v_pk_fma_f32 v[32:33], v[32:33], v[208:209], v[66:67] op_sel_hi:[0,1,1]
	s_nop 0
	v_pk_mul_f32 v[66:67], v[210:211], v[34:35] op_sel:[1,1] op_sel_hi:[0,1] neg_lo:[0,1]
	v_pk_fma_f32 v[34:35], v[210:211], v[34:35], v[66:67] op_sel_hi:[1,0,1]
	s_nop 0
	v_pk_mul_f32 v[66:67], v[36:37], v[212:213] op_sel:[1,1] op_sel_hi:[1,0] neg_lo:[1,0]
	s_nop 0
	v_pk_fma_f32 v[36:37], v[36:37], v[212:213], v[66:67] op_sel_hi:[0,1,1]
	v_pk_add_f32 v[70:71], v[20:21], v[36:37]
	v_pk_add_f32 v[20:21], v[20:21], v[36:37] neg_lo:[0,1] neg_hi:[0,1]
	s_nop 0
	v_pk_mul_f32 v[66:67], v[40:41], v[214:215] op_sel:[1,1] op_sel_hi:[1,0] neg_lo:[1,0]
	s_nop 0
	v_pk_fma_f32 v[40:41], v[40:41], v[214:215], v[66:67] op_sel_hi:[0,1,1]
	v_pk_add_f32 v[36:37], v[22:23], v[40:41]
	v_pk_add_f32 v[22:23], v[22:23], v[40:41] neg_lo:[0,1] neg_hi:[0,1]
	s_nop 0
	v_pk_mul_f32 v[66:67], v[42:43], v[216:217] op_sel:[1,1] op_sel_hi:[1,0] neg_lo:[1,0]
	s_nop 0
	v_pk_fma_f32 v[42:43], v[42:43], v[216:217], v[66:67] op_sel_hi:[0,1,1]
	s_nop 0
	v_pk_mul_f32 v[66:67], v[46:47], v[218:219] op_sel:[1,1] op_sel_hi:[1,0] neg_lo:[1,0]
	s_nop 0
	v_pk_fma_f32 v[46:47], v[46:47], v[218:219], v[66:67] op_sel_hi:[0,1,1]
	s_nop 0
	v_pk_mul_f32 v[66:67], v[44:45], v[220:221] op_sel:[1,1] op_sel_hi:[1,0] neg_lo:[1,0]
	s_nop 0
	v_pk_fma_f32 v[44:45], v[44:45], v[220:221], v[66:67] op_sel_hi:[0,1,1]
	s_nop 0
	v_pk_mul_f32 v[66:67], v[48:49], v[222:223] op_sel:[1,1] op_sel_hi:[1,0] neg_lo:[1,0]
	s_nop 0
	v_pk_fma_f32 v[48:49], v[48:49], v[222:223], v[66:67] op_sel_hi:[0,1,1]
	s_nop 0
	v_pk_mul_f32 v[66:67], v[38:39], v[224:225] op_sel:[1,1] op_sel_hi:[1,0] neg_lo:[1,0]
	s_nop 0
	v_pk_fma_f32 v[38:39], v[38:39], v[224:225], v[66:67] op_sel_hi:[0,1,1]
	v_mov_b32_e32 v50, v226
	v_mov_b32_e32 v51, v227
	v_lshlrev_b32_e32 v190, 3, v16
	v_add_u32_e32 v190, 0x11000, v190
	global_load_dwordx2 v[196:197], v190, s[48:49] offset:-4096
	global_load_dwordx2 v[198:199], v190, s[48:49]
	v_add_u32_e32 v190, 0x2000, v190
	global_load_dwordx2 v[200:201], v190, s[48:49] offset:-4096
	global_load_dwordx2 v[202:203], v190, s[48:49]
	v_add_u32_e32 v190, 0x2000, v190
	global_load_dwordx2 v[204:205], v190, s[48:49] offset:-4096
	global_load_dwordx2 v[206:207], v190, s[48:49]
	v_add_u32_e32 v190, 0x2000, v190
	global_load_dwordx2 v[208:209], v190, s[48:49] offset:-4096
	global_load_dwordx2 v[210:211], v190, s[48:49]
	v_add_u32_e32 v190, 0x2000, v190
	global_load_dwordx2 v[212:213], v190, s[48:49] offset:-4096
	global_load_dwordx2 v[214:215], v190, s[48:49]
	v_add_u32_e32 v190, 0x2000, v190
	global_load_dwordx2 v[216:217], v190, s[48:49] offset:-4096
	global_load_dwordx2 v[218:219], v190, s[48:49]
	v_add_u32_e32 v190, 0x2000, v190
	global_load_dwordx2 v[220:221], v190, s[48:49] offset:-4096
	global_load_dwordx2 v[222:223], v190, s[48:49]
	v_add_u32_e32 v190, 0x2000, v190
	global_load_dwordx2 v[224:225], v190, s[48:49] offset:-4096
	global_load_dwordx2 v[226:227], v190, s[48:49]
	s_nop 0
	v_pk_mul_f32 v[66:67], v[18:19], v[50:51] op_sel:[1,1] op_sel_hi:[1,0] neg_lo:[1,0]
	s_nop 0
	v_pk_fma_f32 v[18:19], v[18:19], v[50:51], v[66:67] op_sel_hi:[0,1,1]
	v_mov_b32_e32 v50, v166
	v_mov_b32_e32 v66, v168
	s_nop 0
	v_pk_mul_f32 v[40:41], v[22:23], v[68:69] op_sel:[1,0] op_sel_hi:[0,0] neg_lo:[1,0]
	v_pk_fma_f32 v[22:23], v[22:23], v[50:51], v[40:41] op_sel_hi:[1,0,1]
	v_pk_add_f32 v[40:41], v[24:25], v[42:43]
	v_pk_add_f32 v[24:25], v[24:25], v[42:43] neg_lo:[0,1] neg_hi:[0,1]
	s_nop 0
	v_pk_mul_f32 v[42:43], v[24:25], v[66:67] op_sel:[1,0] op_sel_hi:[0,0] neg_lo:[1,0]
	v_pk_fma_f32 v[24:25], v[24:25], v[66:67], v[42:43] op_sel_hi:[1,0,1]
	v_pk_add_f32 v[42:43], v[26:27], v[46:47]
	v_pk_add_f32 v[26:27], v[26:27], v[46:47] neg_lo:[0,1] neg_hi:[0,1]
	s_nop 0
	v_pk_mul_f32 v[46:47], v[26:27], v[68:69] op_sel_hi:[1,0]
	s_nop 0
	v_pk_fma_f32 v[26:27], v[26:27], v[50:51], v[46:47] op_sel:[1,0,0] op_sel_hi:[0,0,1] neg_lo:[1,0,0]
	v_pk_add_f32 v[46:47], v[28:29], v[44:45]
	v_pk_add_f32 v[28:29], v[28:29], v[44:45] neg_lo:[0,1] neg_hi:[0,1]
	v_mov_b32_e32 v17, v177
	v_xor_b32_e32 v44, 0x80000000, v29
	v_mov_b32_e32 v45, v28
	v_pk_add_f32 v[28:29], v[30:31], v[48:49]
	v_pk_add_f32 v[30:31], v[30:31], v[48:49] neg_lo:[0,1] neg_hi:[0,1]
	s_nop 0
	v_pk_mul_f32 v[48:49], v[30:31], v[68:69] op_sel_hi:[1,0] neg_lo:[0,1] neg_hi:[0,1]
	s_nop 0
	v_pk_fma_f32 v[30:31], v[30:31], v[50:51], v[48:49] op_sel:[1,0,0] op_sel_hi:[0,0,1] neg_lo:[1,0,0]
	v_pk_add_f32 v[48:49], v[32:33], v[38:39]
	v_pk_add_f32 v[32:33], v[32:33], v[38:39] neg_lo:[0,1] neg_hi:[0,1]
	s_nop 0
	v_pk_mul_f32 v[38:39], v[32:33], v[66:67] op_sel:[1,0] op_sel_hi:[0,0] neg_lo:[1,0]
	s_nop 0
	v_pk_fma_f32 v[32:33], v[32:33], v[66:67], v[38:39] op_sel_hi:[1,0,1] neg_lo:[0,1,0] neg_hi:[0,1,0]
	v_pk_add_f32 v[38:39], v[34:35], v[18:19]
	v_pk_add_f32 v[18:19], v[34:35], v[18:19] neg_lo:[0,1] neg_hi:[0,1]
	s_nop 0
	v_pk_mul_f32 v[34:35], v[18:19], v[68:69] op_sel:[1,0] op_sel_hi:[0,0] neg_lo:[1,0]
	v_mov_b32_e32 v68, v170
	v_pk_fma_f32 v[18:19], v[18:19], v[50:51], v[34:35] op_sel_hi:[1,0,1] neg_lo:[0,1,0] neg_hi:[0,1,0]
	v_pk_add_f32 v[50:51], v[36:37], v[28:29]
	v_pk_add_f32 v[28:29], v[36:37], v[28:29] neg_lo:[0,1] neg_hi:[0,1]
	v_pk_add_f32 v[34:35], v[70:71], v[46:47]
	v_pk_mul_f32 v[36:37], v[28:29], v[66:67] op_sel:[1,0] op_sel_hi:[0,0] neg_lo:[1,0]
	v_pk_add_f32 v[46:47], v[70:71], v[46:47] neg_lo:[0,1] neg_hi:[0,1]
	v_pk_fma_f32 v[28:29], v[28:29], v[66:67], v[36:37] op_sel_hi:[1,0,1]
	v_pk_add_f32 v[36:37], v[40:41], v[48:49]
	v_pk_add_f32 v[40:41], v[40:41], v[48:49] neg_lo:[0,1] neg_hi:[0,1]
	s_nop 0
	v_xor_b32_e32 v48, 0x80000000, v41
	v_mov_b32_e32 v49, v40
	v_pk_add_f32 v[40:41], v[42:43], v[38:39]
	v_pk_add_f32 v[38:39], v[42:43], v[38:39] neg_lo:[0,1] neg_hi:[0,1]
	s_nop 0
	v_pk_mul_f32 v[42:43], v[66:67], v[38:39] op_sel:[0,1] op_sel_hi:[0,0] neg_lo:[0,1]
	v_pk_fma_f32 v[38:39], v[38:39], v[66:67], v[42:43] op_sel_hi:[1,0,1] neg_lo:[0,1,0] neg_hi:[0,1,0]
	v_pk_add_f32 v[42:43], v[34:35], v[36:37]
	v_pk_add_f32 v[34:35], v[34:35], v[36:37] neg_lo:[0,1] neg_hi:[0,1]
	v_pk_add_f32 v[36:37], v[50:51], v[40:41]
	v_pk_add_f32 v[40:41], v[50:51], v[40:41] neg_lo:[0,1] neg_hi:[0,1]
	s_nop 0
	v_xor_b32_e32 v50, 0x80000000, v41
	v_mov_b32_e32 v51, v40
	v_pk_add_f32 v[40:41], v[42:43], v[36:37]
	v_pk_add_f32 v[36:37], v[42:43], v[36:37] neg_lo:[0,1] neg_hi:[0,1]
	v_pk_add_f32 v[42:43], v[34:35], v[50:51]
	v_pk_add_f32 v[34:35], v[34:35], v[50:51] neg_lo:[0,1] neg_hi:[0,1]
	v_pk_add_f32 v[50:51], v[46:47], v[48:49]
	v_pk_add_f32 v[46:47], v[46:47], v[48:49] neg_lo:[0,1] neg_hi:[0,1]
	v_pk_add_f32 v[48:49], v[28:29], v[38:39]
	v_pk_add_f32 v[28:29], v[28:29], v[38:39] neg_lo:[0,1] neg_hi:[0,1]
	s_nop 0
	v_xor_b32_e32 v38, 0x80000000, v29
	v_mov_b32_e32 v39, v28
	v_pk_add_f32 v[28:29], v[50:51], v[48:49]
	v_pk_add_f32 v[48:49], v[50:51], v[48:49] neg_lo:[0,1] neg_hi:[0,1]
	v_pk_add_f32 v[50:51], v[46:47], v[38:39]
	v_pk_add_f32 v[38:39], v[46:47], v[38:39] neg_lo:[0,1] neg_hi:[0,1]
	v_pk_add_f32 v[46:47], v[20:21], v[44:45]
	v_pk_add_f32 v[20:21], v[20:21], v[44:45] neg_lo:[0,1] neg_hi:[0,1]
	v_pk_add_f32 v[44:45], v[22:23], v[30:31]
	v_pk_add_f32 v[22:23], v[22:23], v[30:31] neg_lo:[0,1] neg_hi:[0,1]
	s_nop 0
	v_pk_mul_f32 v[30:31], v[66:67], v[22:23] op_sel:[0,1] op_sel_hi:[0,0] neg_lo:[0,1]
	v_pk_fma_f32 v[22:23], v[66:67], v[22:23], v[30:31] op_sel_hi:[0,1,1]
	v_pk_add_f32 v[30:31], v[24:25], v[32:33]
	v_pk_add_f32 v[24:25], v[24:25], v[32:33] neg_lo:[0,1] neg_hi:[0,1]
	s_nop 0
	v_xor_b32_e32 v32, 0x80000000, v25
	v_mov_b32_e32 v33, v24
	v_pk_add_f32 v[24:25], v[26:27], v[18:19]
	v_pk_add_f32 v[18:19], v[26:27], v[18:19] neg_lo:[0,1] neg_hi:[0,1]
	s_nop 0
	v_pk_mul_f32 v[26:27], v[66:67], v[18:19] op_sel:[0,1] op_sel_hi:[0,0] neg_lo:[0,1]
	v_pk_fma_f32 v[18:19], v[66:67], v[18:19], v[26:27] op_sel_hi:[0,1,1] neg_lo:[1,0,0] neg_hi:[1,0,0]
	v_pk_add_f32 v[26:27], v[46:47], v[30:31]
	v_pk_add_f32 v[30:31], v[46:47], v[30:31] neg_lo:[0,1] neg_hi:[0,1]
	v_pk_add_f32 v[46:47], v[44:45], v[24:25]
	v_pk_add_f32 v[24:25], v[44:45], v[24:25] neg_lo:[0,1] neg_hi:[0,1]
	v_mov_b32_e32 v66, v168
	v_xor_b32_e32 v44, 0x80000000, v25
	v_mov_b32_e32 v45, v24
	v_pk_add_f32 v[24:25], v[26:27], v[46:47]
	v_pk_add_f32 v[26:27], v[26:27], v[46:47] neg_lo:[0,1] neg_hi:[0,1]
	v_pk_add_f32 v[46:47], v[30:31], v[44:45]
	v_pk_add_f32 v[30:31], v[30:31], v[44:45] neg_lo:[0,1] neg_hi:[0,1]
	v_pk_add_f32 v[44:45], v[20:21], v[32:33]
	v_pk_add_f32 v[20:21], v[20:21], v[32:33] neg_lo:[0,1] neg_hi:[0,1]
	v_pk_add_f32 v[32:33], v[22:23], v[18:19]
	v_pk_add_f32 v[18:19], v[22:23], v[18:19] neg_lo:[0,1] neg_hi:[0,1]
	s_nop 0
	v_xor_b32_e32 v22, 0x80000000, v19
	v_mov_b32_e32 v23, v18
	v_pk_add_f32 v[18:19], v[44:45], v[32:33]
	v_pk_add_f32 v[32:33], v[44:45], v[32:33] neg_lo:[0,1] neg_hi:[0,1]
	v_pk_add_f32 v[44:45], v[20:21], v[22:23]
	v_pk_add_f32 v[20:21], v[20:21], v[22:23] neg_lo:[0,1] neg_hi:[0,1]
	ds_write_b64 v10, v[40:41]
	ds_write_b64 v13, v[24:25]
	ds_write_b64 v15, v[28:29]
	ds_write_b64 v52, v[18:19]
	ds_write_b64 v53, v[42:43]
	ds_write_b64 v54, v[46:47]
	ds_write_b64 v55, v[50:51]
	ds_write_b64 v56, v[44:45]
	ds_write_b64 v57, v[36:37]
	ds_write_b64 v58, v[26:27]
	ds_write_b64 v59, v[48:49]
	ds_write_b64 v60, v[32:33]
	ds_write_b64 v61, v[34:35]
	ds_write_b64 v62, v[30:31]
	ds_write_b64 v63, v[38:39]
	ds_write_b64 v64, v[20:21]
	v_mov_b32_e32 v10, v179
	v_mov_b32_e32 v64, v166
	v_lshlrev_b32_e32 v13, 3, v17
	v_lshlrev_b32_e32 v48, 3, v10
	v_add3_u32 v10, 0, v13, v48
	v_xor_b32_e32 v13, 1, v17
	v_xor_b32_e32 v34, 8, v17
	v_xor_b32_e32 v36, 9, v17
	v_lshlrev_b32_e32 v13, 3, v13
	v_xor_b32_e32 v15, 2, v17
	v_xor_b32_e32 v24, 3, v17
	v_xor_b32_e32 v26, 4, v17
	v_xor_b32_e32 v28, 5, v17
	v_xor_b32_e32 v30, 6, v17
	v_xor_b32_e32 v32, 7, v17
	v_lshlrev_b32_e32 v34, 3, v34
	v_lshlrev_b32_e32 v36, 3, v36
	v_xor_b32_e32 v38, 10, v17
	v_xor_b32_e32 v40, 11, v17
	v_xor_b32_e32 v42, 12, v17
	v_xor_b32_e32 v44, 13, v17
	v_xor_b32_e32 v46, 14, v17
	v_xor_b32_e32 v17, 15, v17
	v_add3_u32 v13, 0, v13, v48
	v_lshlrev_b32_e32 v15, 3, v15
	v_lshlrev_b32_e32 v24, 3, v24
	v_lshlrev_b32_e32 v26, 3, v26
	v_lshlrev_b32_e32 v28, 3, v28
	v_lshlrev_b32_e32 v30, 3, v30
	v_lshlrev_b32_e32 v32, 3, v32
	v_add3_u32 v55, 0, v34, v48
	v_add3_u32 v56, 0, v36, v48
	v_lshlrev_b32_e32 v38, 3, v38
	v_lshlrev_b32_e32 v40, 3, v40
	v_lshlrev_b32_e32 v42, 3, v42
	v_lshlrev_b32_e32 v44, 3, v44
	v_lshlrev_b32_e32 v46, 3, v46
	v_lshlrev_b32_e32 v17, 3, v17
	ds_read_b64 v[18:19], v10
	ds_read_b64 v[20:21], v13
	v_add3_u32 v15, 0, v15, v48
	v_add3_u32 v50, 0, v24, v48
	v_add3_u32 v51, 0, v26, v48
	v_add3_u32 v52, 0, v28, v48
	v_add3_u32 v53, 0, v30, v48
	v_add3_u32 v54, 0, v32, v48
	ds_read_b64 v[34:35], v55
	ds_read_b64 v[36:37], v56
	v_add3_u32 v57, 0, v38, v48
	v_add3_u32 v58, 0, v40, v48
	v_add3_u32 v59, 0, v42, v48
	v_add3_u32 v60, 0, v44, v48
	v_add3_u32 v61, 0, v46, v48
	v_add3_u32 v62, 0, v17, v48
	ds_read_b64 v[22:23], v15
	ds_read_b64 v[24:25], v50
	ds_read_b64 v[26:27], v51
	ds_read_b64 v[28:29], v52
	ds_read_b64 v[30:31], v53
	ds_read_b64 v[32:33], v54
	ds_read_b64 v[38:39], v57
	ds_read_b64 v[40:41], v58
	ds_read_b64 v[42:43], v59
	ds_read_b64 v[44:45], v60
	ds_read_b64 v[46:47], v61
	ds_read_b64 v[48:49], v62
	s_waitcnt lgkmcnt(13)
	v_pk_add_f32 v[70:71], v[18:19], v[34:35]
	v_pk_add_f32 v[18:19], v[18:19], v[34:35] neg_lo:[0,1] neg_hi:[0,1]
	s_waitcnt lgkmcnt(12)
	v_pk_add_f32 v[34:35], v[20:21], v[36:37]
	v_pk_add_f32 v[20:21], v[20:21], v[36:37] neg_lo:[0,1] neg_hi:[0,1]
	s_nop 0
	v_pk_mul_f32 v[36:37], v[20:21], v[68:69] op_sel:[1,0] op_sel_hi:[0,0] neg_lo:[1,1] neg_hi:[0,1]
	v_pk_fma_f32 v[20:21], v[20:21], v[64:65], v[36:37] op_sel_hi:[1,0,1]
	s_waitcnt lgkmcnt(5)
	v_pk_add_f32 v[36:37], v[22:23], v[38:39]
	v_pk_add_f32 v[22:23], v[22:23], v[38:39] neg_lo:[0,1] neg_hi:[0,1]
	s_nop 0
	v_pk_mul_f32 v[38:39], v[22:23], v[66:67] op_sel:[1,0] op_sel_hi:[0,0] neg_lo:[1,1] neg_hi:[0,1]
	v_pk_fma_f32 v[22:23], v[22:23], v[66:67], v[38:39] op_sel_hi:[1,0,1]
	s_waitcnt lgkmcnt(4)
	v_pk_add_f32 v[38:39], v[24:25], v[40:41]
	v_pk_add_f32 v[24:25], v[24:25], v[40:41] neg_lo:[0,1] neg_hi:[0,1]
	s_nop 0
	v_pk_mul_f32 v[40:41], v[24:25], v[68:69] op_sel_hi:[1,0]
	s_nop 0
	v_pk_fma_f32 v[24:25], v[24:25], v[64:65], v[40:41] op_sel:[1,0,0] op_sel_hi:[0,0,1] neg_lo:[1,1,0] neg_hi:[0,1,0]
	s_waitcnt lgkmcnt(3)
	v_pk_add_f32 v[40:41], v[26:27], v[42:43]
	v_pk_add_f32 v[26:27], v[26:27], v[42:43] neg_lo:[0,1] neg_hi:[0,1]
	s_nop 0
	v_xor_b32_e32 v73, 0x80000000, v26
	v_mov_b32_e32 v72, v27
	s_waitcnt lgkmcnt(2)
	v_pk_add_f32 v[26:27], v[28:29], v[44:45]
	v_pk_add_f32 v[28:29], v[28:29], v[44:45] neg_lo:[0,1] neg_hi:[0,1]
	s_nop 0
	v_pk_mul_f32 v[42:43], v[28:29], v[68:69] op_sel_hi:[1,0] neg_lo:[0,1] neg_hi:[0,1]
	s_nop 0
	v_pk_fma_f32 v[28:29], v[28:29], v[64:65], v[42:43] op_sel:[1,0,0] op_sel_hi:[0,0,1] neg_lo:[1,1,0] neg_hi:[0,1,0]
	s_waitcnt lgkmcnt(1)
	v_pk_add_f32 v[42:43], v[30:31], v[46:47]
	v_pk_add_f32 v[30:31], v[30:31], v[46:47] neg_lo:[0,1] neg_hi:[0,1]
	s_nop 0
	v_pk_mul_f32 v[44:45], v[30:31], v[66:67] op_sel:[1,0] op_sel_hi:[0,0] neg_lo:[1,1] neg_hi:[0,1]
	s_nop 0
	v_pk_fma_f32 v[30:31], v[30:31], v[66:67], v[44:45] op_sel_hi:[1,0,1] neg_lo:[0,1,0] neg_hi:[0,1,0]
	s_waitcnt lgkmcnt(0)
	v_pk_add_f32 v[44:45], v[32:33], v[48:49]
	v_pk_add_f32 v[32:33], v[32:33], v[48:49] neg_lo:[0,1] neg_hi:[0,1]
	v_pk_add_f32 v[48:49], v[34:35], v[26:27]
	v_pk_add_f32 v[26:27], v[34:35], v[26:27] neg_lo:[0,1] neg_hi:[0,1]
	s_nop 0
	v_pk_mul_f32 v[34:35], v[26:27], v[66:67] op_sel:[1,0] op_sel_hi:[0,0] neg_lo:[1,1] neg_hi:[0,1]
	v_pk_fma_f32 v[26:27], v[26:27], v[66:67], v[34:35] op_sel_hi:[1,0,1]
	v_pk_add_f32 v[34:35], v[36:37], v[42:43]
	v_pk_add_f32 v[36:37], v[36:37], v[42:43] neg_lo:[0,1] neg_hi:[0,1]
	v_pk_mul_f32 v[46:47], v[32:33], v[68:69] op_sel:[1,0] op_sel_hi:[0,0] neg_lo:[1,1] neg_hi:[0,1]
	v_xor_b32_e32 v43, 0x80000000, v36
	v_mov_b32_e32 v42, v37
	v_pk_add_f32 v[36:37], v[38:39], v[44:45]
	v_pk_add_f32 v[38:39], v[38:39], v[44:45] neg_lo:[0,1] neg_hi:[0,1]
	v_pk_fma_f32 v[46:47], v[32:33], v[64:65], v[46:47] op_sel_hi:[1,0,1] neg_lo:[0,1,0] neg_hi:[0,1,0]
	v_pk_add_f32 v[32:33], v[70:71], v[40:41]
	v_pk_mul_f32 v[44:45], v[38:39], v[66:67] op_sel:[1,0] op_sel_hi:[0,0] neg_lo:[1,1] neg_hi:[0,1]
	v_pk_add_f32 v[40:41], v[70:71], v[40:41] neg_lo:[0,1] neg_hi:[0,1]
	v_pk_fma_f32 v[38:39], v[38:39], v[66:67], v[44:45] op_sel_hi:[1,0,1] neg_lo:[0,1,0] neg_hi:[0,1,0]
	v_pk_add_f32 v[44:45], v[32:33], v[34:35]
	v_pk_add_f32 v[32:33], v[32:33], v[34:35] neg_lo:[0,1] neg_hi:[0,1]
	v_pk_add_f32 v[34:35], v[48:49], v[36:37]
	v_pk_add_f32 v[36:37], v[48:49], v[36:37] neg_lo:[0,1] neg_hi:[0,1]
	v_pk_add_f32 v[64:65], v[44:45], v[34:35]
	v_xor_b32_e32 v49, 0x80000000, v36
	v_mov_b32_e32 v48, v37
	v_pk_add_f32 v[36:37], v[44:45], v[34:35] neg_lo:[0,1] neg_hi:[0,1]
	v_pk_add_f32 v[68:69], v[32:33], v[48:49]
	v_pk_add_f32 v[44:45], v[32:33], v[48:49] neg_lo:[0,1] neg_hi:[0,1]
	v_pk_add_f32 v[32:33], v[40:41], v[42:43]
	v_pk_add_f32 v[34:35], v[40:41], v[42:43] neg_lo:[0,1] neg_hi:[0,1]
	v_pk_add_f32 v[40:41], v[26:27], v[38:39]
	v_pk_add_f32 v[26:27], v[26:27], v[38:39] neg_lo:[0,1] neg_hi:[0,1]
	v_pk_add_f32 v[42:43], v[32:33], v[40:41] neg_lo:[0,1] neg_hi:[0,1]
	v_xor_b32_e32 v39, 0x80000000, v26
	v_mov_b32_e32 v38, v27
	v_pk_add_f32 v[26:27], v[32:33], v[40:41]
	v_pk_add_f32 v[40:41], v[20:21], v[28:29]
	v_pk_add_f32 v[20:21], v[20:21], v[28:29] neg_lo:[0,1] neg_hi:[0,1]
	v_pk_add_f32 v[32:33], v[34:35], v[38:39]
	v_pk_mul_f32 v[28:29], v[66:67], v[20:21] op_sel:[0,1] op_sel_hi:[0,0] neg_lo:[1,1] neg_hi:[1,0]
	v_pk_fma_f32 v[20:21], v[66:67], v[20:21], v[28:29] op_sel_hi:[0,1,1]
	v_pk_add_f32 v[28:29], v[22:23], v[30:31]
	v_pk_add_f32 v[22:23], v[22:23], v[30:31] neg_lo:[0,1] neg_hi:[0,1]
	v_pk_add_f32 v[38:39], v[34:35], v[38:39] neg_lo:[0,1] neg_hi:[0,1]
	v_xor_b32_e32 v31, 0x80000000, v22
	v_mov_b32_e32 v30, v23
	v_pk_add_f32 v[22:23], v[24:25], v[46:47]
	v_pk_add_f32 v[24:25], v[24:25], v[46:47] neg_lo:[0,1] neg_hi:[0,1]
	v_pk_add_f32 v[34:35], v[18:19], v[72:73]
	v_pk_mul_f32 v[46:47], v[66:67], v[24:25] op_sel:[0,1] op_sel_hi:[0,0] neg_lo:[1,1] neg_hi:[1,0]
	v_pk_fma_f32 v[24:25], v[66:67], v[24:25], v[46:47] op_sel_hi:[0,1,1] neg_lo:[1,0,0] neg_hi:[1,0,0]
	v_pk_add_f32 v[46:47], v[34:35], v[28:29]
	v_pk_add_f32 v[28:29], v[34:35], v[28:29] neg_lo:[0,1] neg_hi:[0,1]
	v_pk_add_f32 v[34:35], v[40:41], v[22:23]
	v_pk_add_f32 v[22:23], v[40:41], v[22:23] neg_lo:[0,1] neg_hi:[0,1]
	v_pk_add_f32 v[18:19], v[18:19], v[72:73] neg_lo:[0,1] neg_hi:[0,1]
	v_pk_add_f32 v[66:67], v[28:29], v[22:23] op_sel:[0,1] op_sel_hi:[1,0] neg_hi:[0,1]
	v_pk_add_f32 v[48:49], v[28:29], v[22:23] op_sel:[0,1] op_sel_hi:[1,0] neg_lo:[0,1]
	v_pk_add_f32 v[28:29], v[18:19], v[30:31]
	v_pk_add_f32 v[18:19], v[18:19], v[30:31] neg_lo:[0,1] neg_hi:[0,1]
	v_pk_add_f32 v[30:31], v[20:21], v[24:25]
	v_pk_add_f32 v[20:21], v[20:21], v[24:25] neg_lo:[0,1] neg_hi:[0,1]
	v_pk_add_f32 v[22:23], v[46:47], v[34:35]
	v_xor_b32_e32 v25, 0x80000000, v20
	v_mov_b32_e32 v24, v21
	s_waitcnt vmcnt(0)
	v_pk_add_f32 v[40:41], v[46:47], v[34:35] neg_lo:[0,1] neg_hi:[0,1]
	v_pk_add_f32 v[34:35], v[18:19], v[24:25]
	v_pk_add_f32 v[18:19], v[18:19], v[24:25] neg_lo:[0,1] neg_hi:[0,1]
	v_pk_add_f32 v[70:71], v[28:29], v[30:31]
	v_pk_add_f32 v[46:47], v[28:29], v[30:31] neg_lo:[0,1] neg_hi:[0,1]
	s_nop 0
	v_pk_mul_f32 v[24:25], v[64:65], v[196:197] op_sel:[1,1] op_sel_hi:[1,0] neg_lo:[1,0]
	s_nop 0
	v_pk_fma_f32 v[20:21], v[64:65], v[196:197], v[24:25] op_sel_hi:[0,1,1]
	s_nop 0
	v_pk_mul_f32 v[28:29], v[198:199], v[22:23] op_sel:[1,1] op_sel_hi:[0,1] neg_lo:[0,1]
	v_pk_fma_f32 v[22:23], v[198:199], v[22:23], v[28:29] op_sel_hi:[1,0,1]
	s_nop 0
	v_pk_mul_f32 v[28:29], v[26:27], v[200:201] op_sel:[1,1] op_sel_hi:[1,0] neg_lo:[1,0]
	s_nop 0
	v_pk_fma_f32 v[24:25], v[26:27], v[200:201], v[28:29] op_sel_hi:[0,1,1]
	s_nop 0
	v_pk_mul_f32 v[28:29], v[202:203], v[70:71] op_sel:[1,1] op_sel_hi:[0,1] neg_lo:[0,1]
	v_pk_fma_f32 v[26:27], v[202:203], v[70:71], v[28:29] op_sel_hi:[1,0,1]
	s_nop 0
	v_pk_mul_f32 v[30:31], v[68:69], v[204:205] op_sel:[1,1] op_sel_hi:[1,0] neg_lo:[1,0]
	s_nop 0
	v_pk_fma_f32 v[28:29], v[68:69], v[204:205], v[30:31] op_sel_hi:[0,1,1]
	s_nop 0
	v_pk_mul_f32 v[64:65], v[206:207], v[66:67] op_sel:[1,1] op_sel_hi:[0,1] neg_lo:[0,1]
	v_pk_fma_f32 v[30:31], v[206:207], v[66:67], v[64:65] op_sel_hi:[1,0,1]
	s_nop 0
	v_pk_mul_f32 v[66:67], v[32:33], v[208:209] op_sel:[1,1] op_sel_hi:[1,0] neg_lo:[1,0]
	s_nop 0
	v_pk_fma_f32 v[32:33], v[32:33], v[208:209], v[66:67] op_sel_hi:[0,1,1]
	s_nop 0
	v_pk_mul_f32 v[66:67], v[210:211], v[34:35] op_sel:[1,1] op_sel_hi:[0,1] neg_lo:[0,1]
	v_pk_fma_f32 v[34:35], v[210:211], v[34:35], v[66:67] op_sel_hi:[1,0,1]
	s_nop 0
	v_pk_mul_f32 v[66:67], v[36:37], v[212:213] op_sel:[1,1] op_sel_hi:[1,0] neg_lo:[1,0]
	s_nop 0
	v_pk_fma_f32 v[36:37], v[36:37], v[212:213], v[66:67] op_sel_hi:[0,1,1]
	v_pk_add_f32 v[68:69], v[20:21], v[36:37]
	v_pk_add_f32 v[20:21], v[20:21], v[36:37] neg_lo:[0,1] neg_hi:[0,1]
	s_nop 0
	v_pk_mul_f32 v[66:67], v[40:41], v[214:215] op_sel:[1,1] op_sel_hi:[1,0] neg_lo:[1,0]
	s_nop 0
	v_pk_fma_f32 v[40:41], v[40:41], v[214:215], v[66:67] op_sel_hi:[0,1,1]
	v_pk_add_f32 v[36:37], v[22:23], v[40:41]
	v_pk_add_f32 v[22:23], v[22:23], v[40:41] neg_lo:[0,1] neg_hi:[0,1]
	s_nop 0
	v_pk_mul_f32 v[66:67], v[42:43], v[216:217] op_sel:[1,1] op_sel_hi:[1,0] neg_lo:[1,0]
	s_nop 0
	v_pk_fma_f32 v[42:43], v[42:43], v[216:217], v[66:67] op_sel_hi:[0,1,1]
	s_nop 0
	v_pk_mul_f32 v[66:67], v[46:47], v[218:219] op_sel:[1,1] op_sel_hi:[1,0] neg_lo:[1,0]
	s_nop 0
	v_pk_fma_f32 v[46:47], v[46:47], v[218:219], v[66:67] op_sel_hi:[0,1,1]
	s_nop 0
	v_pk_mul_f32 v[66:67], v[44:45], v[220:221] op_sel:[1,1] op_sel_hi:[1,0] neg_lo:[1,0]
	s_nop 0
	v_pk_fma_f32 v[44:45], v[44:45], v[220:221], v[66:67] op_sel_hi:[0,1,1]
	s_nop 0
	v_pk_mul_f32 v[66:67], v[48:49], v[222:223] op_sel:[1,1] op_sel_hi:[1,0] neg_lo:[1,0]
	s_nop 0
	v_pk_fma_f32 v[48:49], v[48:49], v[222:223], v[66:67] op_sel_hi:[0,1,1]
	s_nop 0
	v_pk_mul_f32 v[66:67], v[38:39], v[224:225] op_sel:[1,1] op_sel_hi:[1,0] neg_lo:[1,0]
	s_nop 0
	v_pk_fma_f32 v[38:39], v[38:39], v[224:225], v[66:67] op_sel_hi:[0,1,1]
	s_nop 0
	v_pk_mul_f32 v[64:65], v[18:19], v[226:227] op_sel:[1,1] op_sel_hi:[1,0] neg_lo:[1,0]
	v_mov_b32_e32 v66, v170
	v_pk_fma_f32 v[16:17], v[18:19], v[226:227], v[64:65] op_sel_hi:[0,1,1]
	v_mov_b32_e32 v64, v168
	v_mov_b32_e32 v18, v166
	s_nop 0
	s_nop 0
	v_pk_mul_f32 v[40:41], v[22:23], v[66:67] op_sel:[1,0] op_sel_hi:[0,0] neg_lo:[1,0]
	v_mov_b32_e32 v19, v172
	s_nop 0
	v_pk_fma_f32 v[22:23], v[22:23], v[18:19], v[40:41] op_sel_hi:[1,0,1]
	v_pk_add_f32 v[40:41], v[24:25], v[42:43]
	v_pk_add_f32 v[24:25], v[24:25], v[42:43] neg_lo:[0,1] neg_hi:[0,1]
	s_nop 0
	v_pk_mul_f32 v[42:43], v[24:25], v[64:65] op_sel:[1,0] op_sel_hi:[0,0] neg_lo:[1,0]
	s_nop 0
	v_pk_fma_f32 v[24:25], v[24:25], v[64:65], v[42:43] op_sel_hi:[1,0,1]
	v_pk_add_f32 v[42:43], v[26:27], v[46:47]
	v_pk_add_f32 v[26:27], v[26:27], v[46:47] neg_lo:[0,1] neg_hi:[0,1]
	s_nop 0
	v_pk_mul_f32 v[46:47], v[26:27], v[66:67] op_sel_hi:[1,0]
	s_nop 0
	v_pk_fma_f32 v[26:27], v[26:27], v[18:19], v[46:47] op_sel:[1,0,0] op_sel_hi:[0,0,1] neg_lo:[1,0,0]
	v_pk_add_f32 v[46:47], v[28:29], v[44:45]
	v_pk_add_f32 v[28:29], v[28:29], v[44:45] neg_lo:[0,1] neg_hi:[0,1]
	s_nop 0
	v_xor_b32_e32 v44, 0x80000000, v29
	v_mov_b32_e32 v45, v28
	v_pk_add_f32 v[28:29], v[30:31], v[48:49]
	v_pk_add_f32 v[30:31], v[30:31], v[48:49] neg_lo:[0,1] neg_hi:[0,1]
	s_nop 0
	v_pk_mul_f32 v[48:49], v[30:31], v[66:67] op_sel_hi:[1,0] neg_lo:[0,1] neg_hi:[0,1]
	s_nop 0
	v_pk_fma_f32 v[30:31], v[30:31], v[18:19], v[48:49] op_sel:[1,0,0] op_sel_hi:[0,0,1] neg_lo:[1,0,0]
	v_pk_add_f32 v[48:49], v[32:33], v[38:39]
	v_pk_add_f32 v[32:33], v[32:33], v[38:39] neg_lo:[0,1] neg_hi:[0,1]
	s_nop 0
	v_pk_mul_f32 v[38:39], v[32:33], v[64:65] op_sel:[1,0] op_sel_hi:[0,0] neg_lo:[1,0]
	s_nop 0
	v_pk_fma_f32 v[32:33], v[32:33], v[64:65], v[38:39] op_sel_hi:[1,0,1] neg_lo:[0,1,0] neg_hi:[0,1,0]
	v_pk_add_f32 v[38:39], v[34:35], v[16:17]
	v_pk_add_f32 v[16:17], v[34:35], v[16:17] neg_lo:[0,1] neg_hi:[0,1]
	s_nop 0
	v_pk_mul_f32 v[34:35], v[16:17], v[66:67] op_sel:[1,0] op_sel_hi:[0,0] neg_lo:[1,0]
	s_nop 0
	v_pk_fma_f32 v[16:17], v[16:17], v[18:19], v[34:35] op_sel_hi:[1,0,1] neg_lo:[0,1,0] neg_hi:[0,1,0]
	v_pk_add_f32 v[18:19], v[68:69], v[46:47]
	v_pk_add_f32 v[34:35], v[68:69], v[46:47] neg_lo:[0,1] neg_hi:[0,1]
	v_pk_add_f32 v[46:47], v[36:37], v[28:29]
	v_pk_add_f32 v[28:29], v[36:37], v[28:29] neg_lo:[0,1] neg_hi:[0,1]
	s_nop 0
	v_pk_mul_f32 v[36:37], v[28:29], v[64:65] op_sel:[1,0] op_sel_hi:[0,0] neg_lo:[1,0]
	s_nop 0
	v_pk_fma_f32 v[28:29], v[28:29], v[64:65], v[36:37] op_sel_hi:[1,0,1]
	v_pk_add_f32 v[36:37], v[40:41], v[48:49]
	v_pk_add_f32 v[40:41], v[40:41], v[48:49] neg_lo:[0,1] neg_hi:[0,1]
	s_nop 0
	v_xor_b32_e32 v48, 0x80000000, v41
	v_mov_b32_e32 v49, v40
	v_pk_add_f32 v[40:41], v[42:43], v[38:39]
	v_pk_add_f32 v[38:39], v[42:43], v[38:39] neg_lo:[0,1] neg_hi:[0,1]
	s_nop 0
	v_pk_mul_f32 v[42:43], v[64:65], v[38:39] op_sel:[0,1] op_sel_hi:[0,0] neg_lo:[0,1]
	v_pk_fma_f32 v[38:39], v[38:39], v[64:65], v[42:43] op_sel_hi:[1,0,1] neg_lo:[0,1,0] neg_hi:[0,1,0]
	v_pk_add_f32 v[42:43], v[18:19], v[36:37]
	v_pk_add_f32 v[18:19], v[18:19], v[36:37] neg_lo:[0,1] neg_hi:[0,1]
	v_pk_add_f32 v[36:37], v[46:47], v[40:41]
	v_pk_add_f32 v[40:41], v[46:47], v[40:41] neg_lo:[0,1] neg_hi:[0,1]
	s_nop 0
	v_xor_b32_e32 v46, 0x80000000, v41
	v_mov_b32_e32 v47, v40
	v_pk_add_f32 v[40:41], v[42:43], v[36:37]
	v_pk_add_f32 v[36:37], v[42:43], v[36:37] neg_lo:[0,1] neg_hi:[0,1]
	v_pk_add_f32 v[42:43], v[18:19], v[46:47]
	v_pk_add_f32 v[18:19], v[18:19], v[46:47] neg_lo:[0,1] neg_hi:[0,1]
	v_pk_add_f32 v[46:47], v[34:35], v[48:49]
	v_pk_add_f32 v[34:35], v[34:35], v[48:49] neg_lo:[0,1] neg_hi:[0,1]
	v_pk_add_f32 v[48:49], v[28:29], v[38:39]
	v_pk_add_f32 v[28:29], v[28:29], v[38:39] neg_lo:[0,1] neg_hi:[0,1]
	s_nop 0
	v_xor_b32_e32 v38, 0x80000000, v29
	v_mov_b32_e32 v39, v28
	v_pk_add_f32 v[28:29], v[46:47], v[48:49]
	v_pk_add_f32 v[46:47], v[46:47], v[48:49] neg_lo:[0,1] neg_hi:[0,1]
	v_pk_add_f32 v[48:49], v[34:35], v[38:39]
	v_pk_add_f32 v[34:35], v[34:35], v[38:39] neg_lo:[0,1] neg_hi:[0,1]
	v_pk_add_f32 v[38:39], v[20:21], v[44:45]
	v_pk_add_f32 v[20:21], v[20:21], v[44:45] neg_lo:[0,1] neg_hi:[0,1]
	v_pk_add_f32 v[44:45], v[22:23], v[30:31]
	v_pk_add_f32 v[22:23], v[22:23], v[30:31] neg_lo:[0,1] neg_hi:[0,1]
	s_nop 0
	v_pk_mul_f32 v[30:31], v[64:65], v[22:23] op_sel:[0,1] op_sel_hi:[0,0] neg_lo:[0,1]
	v_pk_fma_f32 v[22:23], v[64:65], v[22:23], v[30:31] op_sel_hi:[0,1,1]
	v_pk_add_f32 v[30:31], v[24:25], v[32:33]
	v_pk_add_f32 v[24:25], v[24:25], v[32:33] neg_lo:[0,1] neg_hi:[0,1]
	s_nop 0
	v_xor_b32_e32 v32, 0x80000000, v25
	v_mov_b32_e32 v33, v24
	v_pk_add_f32 v[24:25], v[26:27], v[16:17]
	v_pk_add_f32 v[16:17], v[26:27], v[16:17] neg_lo:[0,1] neg_hi:[0,1]
	s_nop 0
	v_pk_mul_f32 v[26:27], v[64:65], v[16:17] op_sel:[0,1] op_sel_hi:[0,0] neg_lo:[0,1]
	v_pk_fma_f32 v[16:17], v[64:65], v[16:17], v[26:27] op_sel_hi:[0,1,1] neg_lo:[1,0,0] neg_hi:[1,0,0]
	v_pk_add_f32 v[26:27], v[38:39], v[30:31]
	v_pk_add_f32 v[30:31], v[38:39], v[30:31] neg_lo:[0,1] neg_hi:[0,1]
	v_pk_add_f32 v[38:39], v[44:45], v[24:25]
	v_pk_add_f32 v[24:25], v[44:45], v[24:25] neg_lo:[0,1] neg_hi:[0,1]
	s_nop 0
	v_xor_b32_e32 v44, 0x80000000, v25
	v_mov_b32_e32 v45, v24
	v_pk_add_f32 v[24:25], v[26:27], v[38:39]
	v_pk_add_f32 v[26:27], v[26:27], v[38:39] neg_lo:[0,1] neg_hi:[0,1]
	v_pk_add_f32 v[38:39], v[30:31], v[44:45]
	v_pk_add_f32 v[30:31], v[30:31], v[44:45] neg_lo:[0,1] neg_hi:[0,1]
	v_pk_add_f32 v[44:45], v[20:21], v[32:33]
	v_pk_add_f32 v[20:21], v[20:21], v[32:33] neg_lo:[0,1] neg_hi:[0,1]
	v_pk_add_f32 v[32:33], v[22:23], v[16:17]
	v_pk_add_f32 v[16:17], v[22:23], v[16:17] neg_lo:[0,1] neg_hi:[0,1]
	s_nop 0
	v_xor_b32_e32 v22, 0x80000000, v17
	v_mov_b32_e32 v23, v16
	v_pk_add_f32 v[16:17], v[44:45], v[32:33]
	v_pk_add_f32 v[32:33], v[44:45], v[32:33] neg_lo:[0,1] neg_hi:[0,1]
	v_pk_add_f32 v[44:45], v[20:21], v[22:23]
	v_pk_add_f32 v[20:21], v[20:21], v[22:23] neg_lo:[0,1] neg_hi:[0,1]
	ds_write_b64 v10, v[40:41]
	ds_write_b64 v13, v[24:25]
	ds_write_b64 v15, v[28:29]
	ds_write_b64 v50, v[16:17]
	ds_write_b64 v51, v[42:43]
	ds_write_b64 v52, v[38:39]
	ds_write_b64 v53, v[48:49]
	ds_write_b64 v54, v[44:45]
	ds_write_b64 v55, v[36:37]
	ds_write_b64 v56, v[26:27]
	ds_write_b64 v57, v[46:47]
	ds_write_b64 v58, v[32:33]
	ds_write_b64 v59, v[18:19]
	ds_write_b64 v60, v[30:31]
	ds_write_b64 v61, v[34:35]
	ds_write_b64 v62, v[20:21]
	v_mov_b32_e32 v10, v176
	v_mov_b32_e32 v50, v173
	s_waitcnt lgkmcnt(0)
	s_barrier
	v_add_u32_e32 v13, v50, v10
	v_lshl_add_u32 v13, v13, 3, 0
	ds_read2_b64 v[16:19], v13 offset1:16
	v_xad_u32 v15, v50, 1, v10
	v_lshl_add_u32 v15, v15, 3, 0
	s_waitcnt lgkmcnt(0)
	v_pk_fma_f32 v[16:17], v[16:17], 0, v[16:17] op_sel:[1,0,0] op_sel_hi:[0,0,1] neg_hi:[1,0,0]
	v_pk_fma_f32 v[22:23], v[182:183], s[92:93], v[182:183] op_sel:[1,0,0] op_sel_hi:[0,1,1]
	v_pk_mul_f32 v[24:25], v[22:23], v[18:19] op_sel:[1,1] op_sel_hi:[1,0] neg_hi:[0,1]
	s_nop 0
	v_pk_fma_f32 v[18:19], v[18:19], v[22:23], v[24:25] op_sel_hi:[1,0,1]
	v_pk_mul_f32 v[24:25], v[182:183], v[22:23] op_sel:[1,1] op_sel_hi:[0,1] neg_lo:[0,1]
	v_pk_fma_f32 v[26:27], v[182:183], v[22:23], v[24:25] op_sel_hi:[1,0,1]
	ds_read2_b64 v[22:25], v15 offset0:32 offset1:48
	s_waitcnt lgkmcnt(0)
	v_pk_mul_f32 v[28:29], v[22:23], v[26:27] op_sel:[1,1] op_sel_hi:[0,1] neg_hi:[1,0]
	s_nop 0
	v_pk_fma_f32 v[22:23], v[22:23], v[26:27], v[28:29] op_sel_hi:[1,0,1]
	v_pk_mul_f32 v[28:29], v[182:183], v[26:27] op_sel:[1,1] op_sel_hi:[0,1] neg_lo:[0,1]
	v_pk_fma_f32 v[26:27], v[182:183], v[26:27], v[28:29] op_sel_hi:[1,0,1]
	s_nop 0
	v_pk_mul_f32 v[28:29], v[24:25], v[26:27] op_sel:[1,1] op_sel_hi:[0,1] neg_hi:[1,0]
	s_nop 0
	v_pk_fma_f32 v[24:25], v[24:25], v[26:27], v[28:29] op_sel_hi:[1,0,1]
	v_pk_mul_f32 v[28:29], v[182:183], v[26:27] op_sel:[1,1] op_sel_hi:[0,1] neg_lo:[0,1]
	v_pk_fma_f32 v[26:27], v[182:183], v[26:27], v[28:29] op_sel_hi:[1,0,1]
	v_xad_u32 v28, v50, 2, v10
	v_lshl_add_u32 v51, v28, 3, 0
	ds_read2_b64 v[28:31], v51 offset0:64 offset1:80
	v_pk_mul_f32 v[32:33], v[182:183], v[26:27] op_sel:[1,1] op_sel_hi:[0,1] neg_lo:[0,1]
	s_waitcnt lgkmcnt(0)
	v_pk_mul_f32 v[34:35], v[28:29], v[26:27] op_sel:[1,1] op_sel_hi:[0,1] neg_hi:[1,0]
	s_nop 0
	v_pk_fma_f32 v[28:29], v[28:29], v[26:27], v[34:35] op_sel_hi:[1,0,1]
	v_pk_fma_f32 v[34:35], v[182:183], v[26:27], v[32:33] op_sel_hi:[1,0,1]
	s_nop 0
	v_pk_mul_f32 v[26:27], v[30:31], v[34:35] op_sel:[1,1] op_sel_hi:[0,1] neg_hi:[1,0]
	v_pk_fma_f32 v[26:27], v[30:31], v[34:35], v[26:27] op_sel_hi:[1,0,1]
	v_xad_u32 v30, v50, 3, v10
	v_lshl_add_u32 v54, v30, 3, 0
	ds_read2_b64 v[30:33], v54 offset0:96 offset1:112
	v_pk_mul_f32 v[36:37], v[182:183], v[34:35] op_sel:[1,1] op_sel_hi:[0,1] neg_lo:[0,1]
	v_pk_fma_f32 v[34:35], v[182:183], v[34:35], v[36:37] op_sel_hi:[1,0,1]
	s_waitcnt lgkmcnt(0)
	v_pk_mul_f32 v[36:37], v[30:31], v[34:35] op_sel:[1,1] op_sel_hi:[0,1] neg_hi:[1,0]
	s_nop 0
	v_pk_fma_f32 v[30:31], v[30:31], v[34:35], v[36:37] op_sel_hi:[1,0,1]
	v_pk_mul_f32 v[36:37], v[182:183], v[34:35] op_sel:[1,1] op_sel_hi:[0,1] neg_lo:[0,1]
	v_pk_fma_f32 v[34:35], v[182:183], v[34:35], v[36:37] op_sel_hi:[1,0,1]
	s_nop 0
	v_pk_mul_f32 v[36:37], v[32:33], v[34:35] op_sel:[1,1] op_sel_hi:[0,1] neg_hi:[1,0]
	s_nop 0
	v_pk_fma_f32 v[32:33], v[32:33], v[34:35], v[36:37] op_sel_hi:[1,0,1]
	v_pk_mul_f32 v[36:37], v[182:183], v[34:35] op_sel:[1,1] op_sel_hi:[0,1] neg_lo:[0,1]
	v_pk_fma_f32 v[38:39], v[182:183], v[34:35], v[36:37] op_sel_hi:[1,0,1]
	v_xad_u32 v34, v50, 4, v10
	v_lshl_add_u32 v55, v34, 3, 0
	ds_read2_b64 v[34:37], v55 offset0:128 offset1:144
	v_pk_mul_f32 v[40:41], v[182:183], v[38:39] op_sel:[1,1] op_sel_hi:[0,1] neg_lo:[0,1]
	s_waitcnt lgkmcnt(0)
	v_pk_mul_f32 v[42:43], v[34:35], v[38:39] op_sel:[1,1] op_sel_hi:[0,1] neg_hi:[1,0]
	s_nop 0
	v_pk_fma_f32 v[34:35], v[34:35], v[38:39], v[42:43] op_sel_hi:[1,0,1]
	v_pk_fma_f32 v[42:43], v[182:183], v[38:39], v[40:41] op_sel_hi:[1,0,1]
	s_nop 0
	v_pk_mul_f32 v[38:39], v[36:37], v[42:43] op_sel:[1,1] op_sel_hi:[0,1] neg_hi:[1,0]
	v_pk_fma_f32 v[36:37], v[36:37], v[42:43], v[38:39] op_sel_hi:[1,0,1]
	v_xad_u32 v38, v50, 5, v10
	v_lshl_add_u32 v56, v38, 3, 0
	ds_read2_b64 v[38:41], v56 offset0:160 offset1:176
	v_pk_mul_f32 v[44:45], v[182:183], v[42:43] op_sel:[1,1] op_sel_hi:[0,1] neg_lo:[0,1]
	v_pk_fma_f32 v[42:43], v[182:183], v[42:43], v[44:45] op_sel_hi:[1,0,1]
	s_waitcnt lgkmcnt(0)
	v_pk_mul_f32 v[44:45], v[38:39], v[42:43] op_sel:[1,1] op_sel_hi:[0,1] neg_hi:[1,0]
	s_nop 0
	v_pk_fma_f32 v[38:39], v[38:39], v[42:43], v[44:45] op_sel_hi:[1,0,1]
	v_pk_mul_f32 v[44:45], v[182:183], v[42:43] op_sel:[1,1] op_sel_hi:[0,1] neg_lo:[0,1]
	v_pk_fma_f32 v[42:43], v[182:183], v[42:43], v[44:45] op_sel_hi:[1,0,1]
	s_nop 0
	v_pk_mul_f32 v[44:45], v[40:41], v[42:43] op_sel:[1,1] op_sel_hi:[0,1] neg_hi:[1,0]
	s_nop 0
	v_pk_fma_f32 v[40:41], v[40:41], v[42:43], v[44:45] op_sel_hi:[1,0,1]
	v_pk_mul_f32 v[44:45], v[182:183], v[42:43] op_sel:[1,1] op_sel_hi:[0,1] neg_lo:[0,1]
	v_pk_fma_f32 v[42:43], v[182:183], v[42:43], v[44:45] op_sel_hi:[1,0,1]
	v_xad_u32 v44, v50, 6, v10
	v_lshl_add_u32 v57, v44, 3, 0
	ds_read2_b64 v[44:47], v57 offset0:192 offset1:208
	v_pk_mul_f32 v[48:49], v[182:183], v[42:43] op_sel:[1,1] op_sel_hi:[0,1] neg_lo:[0,1]
	s_waitcnt lgkmcnt(0)
	v_pk_mul_f32 v[52:53], v[44:45], v[42:43] op_sel:[1,1] op_sel_hi:[0,1] neg_hi:[1,0]
	s_nop 0
	v_pk_fma_f32 v[44:45], v[44:45], v[42:43], v[52:53] op_sel_hi:[1,0,1]
	v_pk_fma_f32 v[52:53], v[182:183], v[42:43], v[48:49] op_sel_hi:[1,0,1]
	s_nop 0
	v_pk_mul_f32 v[42:43], v[46:47], v[52:53] op_sel:[1,1] op_sel_hi:[0,1] neg_hi:[1,0]
	v_pk_fma_f32 v[42:43], v[46:47], v[52:53], v[42:43] op_sel_hi:[1,0,1]
	v_xad_u32 v46, v50, 7, v10
	v_lshl_add_u32 v58, v46, 3, 0
	ds_read2_b64 v[46:49], v58 offset0:224 offset1:240
	v_pk_mul_f32 v[60:61], v[182:183], v[52:53] op_sel:[1,1] op_sel_hi:[0,1] neg_lo:[0,1]
	v_pk_fma_f32 v[52:53], v[182:183], v[52:53], v[60:61] op_sel_hi:[1,0,1]
	s_waitcnt lgkmcnt(0)
	v_pk_mul_f32 v[60:61], v[46:47], v[52:53] op_sel:[1,1] op_sel_hi:[0,1] neg_hi:[1,0]
	s_nop 0
	v_pk_fma_f32 v[46:47], v[46:47], v[52:53], v[60:61] op_sel_hi:[1,0,1]
	v_pk_mul_f32 v[60:61], v[182:183], v[52:53] op_sel:[1,1] op_sel_hi:[0,1] neg_lo:[0,1]
	v_pk_fma_f32 v[52:53], v[182:183], v[52:53], v[60:61] op_sel_hi:[1,0,1]
	s_nop 0
	v_pk_mul_f32 v[60:61], v[48:49], v[52:53] op_sel:[1,1] op_sel_hi:[0,1] neg_hi:[1,0]
	s_nop 0
	v_pk_fma_f32 v[48:49], v[48:49], v[52:53], v[60:61] op_sel_hi:[1,0,1]
	v_pk_mul_f32 v[60:61], v[182:183], v[52:53] op_sel:[1,1] op_sel_hi:[0,1] neg_lo:[0,1]
	v_pk_fma_f32 v[64:65], v[182:183], v[52:53], v[60:61] op_sel_hi:[1,0,1]
	v_xad_u32 v52, v50, 8, v10
	v_lshl_add_u32 v52, v52, 3, 0
	v_add_u32_e32 v59, 0x800, v52
	ds_read2_b64 v[60:63], v59 offset1:16
	v_pk_mul_f32 v[66:67], v[182:183], v[64:65] op_sel:[1,1] op_sel_hi:[0,1] neg_lo:[0,1]
	v_pk_fma_f32 v[66:67], v[182:183], v[64:65], v[66:67] op_sel_hi:[1,0,1]
	s_waitcnt lgkmcnt(0)
	v_pk_mul_f32 v[52:53], v[60:61], v[64:65] op_sel:[1,1] op_sel_hi:[0,1] neg_hi:[1,0]
	v_pk_fma_f32 v[52:53], v[60:61], v[64:65], v[52:53] op_sel_hi:[1,0,1]
	v_pk_mul_f32 v[60:61], v[62:63], v[66:67] op_sel:[1,1] op_sel_hi:[0,1] neg_hi:[1,0]
	v_pk_fma_f32 v[70:71], v[62:63], v[66:67], v[60:61] op_sel_hi:[1,0,1]
	v_xad_u32 v60, v50, 9, v10
	v_lshl_add_u32 v60, v60, 3, 0
	v_add_u32_e32 v60, 0x800, v60
	ds_read2_b64 v[62:65], v60 offset0:32 offset1:48
	v_pk_mul_f32 v[68:69], v[182:183], v[66:67] op_sel:[1,1] op_sel_hi:[0,1] neg_lo:[0,1]
	v_pk_fma_f32 v[66:67], v[182:183], v[66:67], v[68:69] op_sel_hi:[1,0,1]
	s_waitcnt lgkmcnt(0)
	v_pk_mul_f32 v[68:69], v[62:63], v[66:67] op_sel:[1,1] op_sel_hi:[0,1] neg_hi:[1,0]
	s_nop 0
	v_pk_fma_f32 v[72:73], v[62:63], v[66:67], v[68:69] op_sel_hi:[1,0,1]
	v_pk_mul_f32 v[62:63], v[182:183], v[66:67] op_sel:[1,1] op_sel_hi:[0,1] neg_lo:[0,1]
	v_pk_fma_f32 v[62:63], v[182:183], v[66:67], v[62:63] op_sel_hi:[1,0,1]
	s_nop 0
	v_pk_mul_f32 v[66:67], v[64:65], v[62:63] op_sel:[1,1] op_sel_hi:[0,1] neg_hi:[1,0]
	s_nop 0
	v_pk_fma_f32 v[74:75], v[64:65], v[62:63], v[66:67] op_sel_hi:[1,0,1]
	v_pk_mul_f32 v[64:65], v[182:183], v[62:63] op_sel:[1,1] op_sel_hi:[0,1] neg_lo:[0,1]
	v_pk_fma_f32 v[66:67], v[182:183], v[62:63], v[64:65] op_sel_hi:[1,0,1]
	v_xad_u32 v61, v50, 10, v10
	v_lshl_add_u32 v61, v61, 3, 0
	v_add_u32_e32 v61, 0x800, v61
	ds_read2_b64 v[62:65], v61 offset0:64 offset1:80
	v_pk_mul_f32 v[68:69], v[182:183], v[66:67] op_sel:[1,1] op_sel_hi:[0,1] neg_lo:[0,1]
	v_pk_fma_f32 v[68:69], v[182:183], v[66:67], v[68:69] op_sel_hi:[1,0,1]
	s_waitcnt lgkmcnt(0)
	v_pk_mul_f32 v[76:77], v[62:63], v[66:67] op_sel:[1,1] op_sel_hi:[0,1] neg_hi:[1,0]
	v_pk_fma_f32 v[76:77], v[62:63], v[66:67], v[76:77] op_sel_hi:[1,0,1]
	v_pk_mul_f32 v[62:63], v[64:65], v[68:69] op_sel:[1,1] op_sel_hi:[0,1] neg_hi:[1,0]
	v_pk_fma_f32 v[78:79], v[64:65], v[68:69], v[62:63] op_sel_hi:[1,0,1]
	v_xad_u32 v62, v50, 11, v10
	v_lshl_add_u32 v62, v62, 3, 0
	v_add_u32_e32 v62, 0x800, v62
	ds_read2_b64 v[64:67], v62 offset0:96 offset1:112
	v_pk_mul_f32 v[80:81], v[182:183], v[68:69] op_sel:[1,1] op_sel_hi:[0,1] neg_lo:[0,1]
	v_pk_fma_f32 v[68:69], v[182:183], v[68:69], v[80:81] op_sel_hi:[1,0,1]
	s_waitcnt lgkmcnt(0)
	v_pk_mul_f32 v[80:81], v[64:65], v[68:69] op_sel:[1,1] op_sel_hi:[0,1] neg_hi:[1,0]
	s_nop 0
	v_pk_fma_f32 v[80:81], v[64:65], v[68:69], v[80:81] op_sel_hi:[1,0,1]
	v_pk_mul_f32 v[64:65], v[182:183], v[68:69] op_sel:[1,1] op_sel_hi:[0,1] neg_lo:[0,1]
	v_pk_fma_f32 v[64:65], v[182:183], v[68:69], v[64:65] op_sel_hi:[1,0,1]
	s_nop 0
	v_pk_mul_f32 v[68:69], v[66:67], v[64:65] op_sel:[1,1] op_sel_hi:[0,1] neg_hi:[1,0]
	s_nop 0
	v_pk_fma_f32 v[82:83], v[66:67], v[64:65], v[68:69] op_sel_hi:[1,0,1]
	v_pk_mul_f32 v[66:67], v[182:183], v[64:65] op_sel:[1,1] op_sel_hi:[0,1] neg_lo:[0,1]
	v_pk_fma_f32 v[68:69], v[182:183], v[64:65], v[66:67] op_sel_hi:[1,0,1]
	v_xad_u32 v63, v50, 12, v10
	v_lshl_add_u32 v63, v63, 3, 0
	v_add_u32_e32 v63, 0x800, v63
	ds_read2_b64 v[64:67], v63 offset0:128 offset1:144
	v_pk_mul_f32 v[84:85], v[182:183], v[68:69] op_sel:[1,1] op_sel_hi:[0,1] neg_lo:[0,1]
	v_pk_fma_f32 v[84:85], v[182:183], v[68:69], v[84:85] op_sel_hi:[1,0,1]
	s_waitcnt lgkmcnt(0)
	v_pk_mul_f32 v[86:87], v[64:65], v[68:69] op_sel:[1,1] op_sel_hi:[0,1] neg_hi:[1,0]
	v_pk_fma_f32 v[86:87], v[64:65], v[68:69], v[86:87] op_sel_hi:[1,0,1]
	v_pk_mul_f32 v[64:65], v[66:67], v[84:85] op_sel:[1,1] op_sel_hi:[0,1] neg_hi:[1,0]
	v_pk_fma_f32 v[88:89], v[66:67], v[84:85], v[64:65] op_sel_hi:[1,0,1]
	v_xad_u32 v64, v50, 13, v10
	v_lshl_add_u32 v64, v64, 3, 0
	v_add_u32_e32 v64, 0x800, v64
	ds_read2_b64 v[66:69], v64 offset0:160 offset1:176
	v_pk_mul_f32 v[90:91], v[182:183], v[84:85] op_sel:[1,1] op_sel_hi:[0,1] neg_lo:[0,1]
	v_pk_fma_f32 v[84:85], v[182:183], v[84:85], v[90:91] op_sel_hi:[1,0,1]
	s_waitcnt lgkmcnt(0)
	v_pk_mul_f32 v[90:91], v[66:67], v[84:85] op_sel:[1,1] op_sel_hi:[0,1] neg_hi:[1,0]
	s_nop 0
	v_pk_fma_f32 v[90:91], v[66:67], v[84:85], v[90:91] op_sel_hi:[1,0,1]
	v_pk_mul_f32 v[66:67], v[182:183], v[84:85] op_sel:[1,1] op_sel_hi:[0,1] neg_lo:[0,1]
	v_pk_fma_f32 v[66:67], v[182:183], v[84:85], v[66:67] op_sel_hi:[1,0,1]
	s_nop 0
	v_pk_mul_f32 v[84:85], v[68:69], v[66:67] op_sel:[1,1] op_sel_hi:[0,1] neg_hi:[1,0]
	s_nop 0
	v_pk_fma_f32 v[84:85], v[68:69], v[66:67], v[84:85] op_sel_hi:[1,0,1]
	v_pk_mul_f32 v[68:69], v[182:183], v[66:67] op_sel:[1,1] op_sel_hi:[0,1] neg_lo:[0,1]
	v_pk_fma_f32 v[92:93], v[182:183], v[66:67], v[68:69] op_sel_hi:[1,0,1]
	v_xad_u32 v65, v50, 14, v10
	v_lshl_add_u32 v65, v65, 3, 0
	v_add_u32_e32 v65, 0x800, v65
	ds_read2_b64 v[66:69], v65 offset0:192 offset1:208
	v_pk_mul_f32 v[94:95], v[182:183], v[92:93] op_sel:[1,1] op_sel_hi:[0,1] neg_lo:[0,1]
	v_xad_u32 v10, v50, 15, v10
	s_waitcnt lgkmcnt(0)
	v_pk_mul_f32 v[96:97], v[66:67], v[92:93] op_sel:[1,1] op_sel_hi:[0,1] neg_hi:[1,0]
	v_lshl_add_u32 v10, v10, 3, 0
	v_pk_fma_f32 v[96:97], v[66:67], v[92:93], v[96:97] op_sel_hi:[1,0,1]
	v_pk_fma_f32 v[92:93], v[182:183], v[92:93], v[94:95] op_sel_hi:[1,0,1]
	s_nop 0
	v_pk_mul_f32 v[66:67], v[68:69], v[92:93] op_sel:[1,1] op_sel_hi:[0,1] neg_hi:[1,0]
	v_add_u32_e32 v101, 0x800, v10
	v_pk_fma_f32 v[94:95], v[68:69], v[92:93], v[66:67] op_sel_hi:[1,0,1]
	ds_read2_b64 v[66:69], v101 offset0:224 offset1:240
	v_pk_mul_f32 v[98:99], v[182:183], v[92:93] op_sel:[1,1] op_sel_hi:[0,1] neg_lo:[0,1]
	v_pk_fma_f32 v[92:93], v[182:183], v[92:93], v[98:99] op_sel_hi:[1,0,1]
	s_waitcnt lgkmcnt(0)
	v_pk_mul_f32 v[98:99], v[66:67], v[92:93] op_sel:[1,1] op_sel_hi:[0,1] neg_hi:[1,0]
	s_nop 0
	v_pk_fma_f32 v[66:67], v[66:67], v[92:93], v[98:99] op_sel_hi:[1,0,1]
	v_pk_mul_f32 v[98:99], v[182:183], v[92:93] op_sel:[1,1] op_sel_hi:[0,1] neg_lo:[0,1]
	v_pk_fma_f32 v[20:21], v[182:183], v[92:93], v[98:99] op_sel_hi:[1,0,1]
	s_nop 0
	v_pk_mul_f32 v[92:93], v[68:69], v[20:21] op_sel:[1,1] op_sel_hi:[0,1] neg_hi:[1,0]
	s_nop 0
	v_pk_fma_f32 v[68:69], v[68:69], v[20:21], v[92:93] op_sel_hi:[1,0,1]
	v_pk_add_f32 v[104:105], v[16:17], v[52:53]
	v_pk_add_f32 v[16:17], v[16:17], v[52:53] neg_lo:[0,1] neg_hi:[0,1]
	v_pk_add_f32 v[52:53], v[18:19], v[70:71]
	v_pk_add_f32 v[18:19], v[18:19], v[70:71] neg_lo:[0,1] neg_hi:[0,1]
	v_mov_b32_e32 v92, v165
	v_mov_b32_e32 v20, v166
	v_mov_b32_e32 v98, v167
	v_mov_b32_e32 v10, v168
	v_mov_b32_e32 v100, v169
	v_mov_b32_e32 v50, v170
	v_mov_b32_e32 v102, v171
	v_mov_b32_e32 v21, v172
	v_pk_mul_f32 v[70:71], v[102:103], v[18:19] op_sel:[0,1] op_sel_hi:[0,0] neg_lo:[0,1]
	v_pk_fma_f32 v[18:19], v[92:93], v[18:19], v[70:71] op_sel_hi:[0,1,1]
	v_pk_add_f32 v[70:71], v[22:23], v[72:73]
	v_pk_add_f32 v[22:23], v[22:23], v[72:73] neg_lo:[0,1] neg_hi:[0,1]
	s_nop 0
	v_pk_mul_f32 v[72:73], v[50:51], v[22:23] op_sel:[0,1] op_sel_hi:[0,0] neg_lo:[0,1]
	v_pk_fma_f32 v[22:23], v[20:21], v[22:23], v[72:73] op_sel_hi:[0,1,1]
	v_pk_add_f32 v[72:73], v[24:25], v[74:75]
	v_pk_add_f32 v[24:25], v[24:25], v[74:75] neg_lo:[0,1] neg_hi:[0,1]
	s_nop 0
	v_pk_mul_f32 v[74:75], v[100:101], v[24:25] op_sel:[0,1] op_sel_hi:[0,0] neg_lo:[0,1]
	v_pk_fma_f32 v[24:25], v[98:99], v[24:25], v[74:75] op_sel_hi:[0,1,1]
	v_pk_add_f32 v[74:75], v[28:29], v[76:77]
	v_pk_add_f32 v[28:29], v[28:29], v[76:77] neg_lo:[0,1] neg_hi:[0,1]
	s_nop 0
	v_pk_mul_f32 v[76:77], v[10:11], v[28:29] op_sel:[0,1] op_sel_hi:[0,0] neg_lo:[0,1]
	v_pk_fma_f32 v[28:29], v[10:11], v[28:29], v[76:77] op_sel_hi:[0,1,1]
	v_pk_add_f32 v[76:77], v[26:27], v[78:79]
	v_pk_add_f32 v[26:27], v[26:27], v[78:79] neg_lo:[0,1] neg_hi:[0,1]
	s_nop 0
	v_pk_mul_f32 v[78:79], v[98:99], v[26:27] op_sel:[0,1] op_sel_hi:[0,0] neg_lo:[0,1]
	v_pk_fma_f32 v[26:27], v[100:101], v[26:27], v[78:79] op_sel_hi:[0,1,1]
	v_pk_add_f32 v[78:79], v[30:31], v[80:81]
	v_pk_add_f32 v[30:31], v[30:31], v[80:81] neg_lo:[0,1] neg_hi:[0,1]
	s_nop 0
	v_pk_mul_f32 v[80:81], v[20:21], v[30:31] op_sel:[0,1] op_sel_hi:[0,0] neg_lo:[0,1]
	v_pk_fma_f32 v[30:31], v[50:51], v[30:31], v[80:81] op_sel_hi:[0,1,1]
	v_pk_add_f32 v[80:81], v[32:33], v[82:83]
	v_pk_add_f32 v[32:33], v[32:33], v[82:83] neg_lo:[0,1] neg_hi:[0,1]
	s_nop 0
	v_pk_mul_f32 v[82:83], v[92:93], v[32:33] op_sel:[0,1] op_sel_hi:[0,0] neg_lo:[0,1]
	v_pk_fma_f32 v[32:33], v[102:103], v[32:33], v[82:83] op_sel_hi:[0,1,1]
	v_pk_add_f32 v[82:83], v[34:35], v[86:87]
	v_pk_add_f32 v[34:35], v[34:35], v[86:87] neg_lo:[0,1] neg_hi:[0,1]
	s_nop 0
	v_xor_b32_e32 v86, 0x80000000, v35
	v_mov_b32_e32 v87, v34
	v_pk_add_f32 v[34:35], v[36:37], v[88:89]
	v_pk_add_f32 v[36:37], v[36:37], v[88:89] neg_lo:[0,1] neg_hi:[0,1]
	s_nop 0
	v_pk_mul_f32 v[88:89], v[92:93], v[36:37] op_sel:[0,1] op_sel_hi:[0,0] neg_lo:[0,1]
	v_pk_fma_f32 v[36:37], v[102:103], v[36:37], v[88:89] op_sel_hi:[0,1,1] neg_lo:[1,0,0] neg_hi:[1,0,0]
	v_pk_add_f32 v[88:89], v[38:39], v[90:91]
	v_pk_add_f32 v[38:39], v[38:39], v[90:91] neg_lo:[0,1] neg_hi:[0,1]
	s_nop 0
	v_pk_mul_f32 v[90:91], v[20:21], v[38:39] op_sel:[0,1] op_sel_hi:[0,0] neg_lo:[0,1]
	v_pk_fma_f32 v[38:39], v[50:51], v[38:39], v[90:91] op_sel_hi:[0,1,1] neg_lo:[1,0,0] neg_hi:[1,0,0]
	v_pk_add_f32 v[90:91], v[40:41], v[84:85]
	v_pk_add_f32 v[40:41], v[40:41], v[84:85] neg_lo:[0,1] neg_hi:[0,1]
	s_nop 0
	v_pk_mul_f32 v[84:85], v[98:99], v[40:41] op_sel:[0,1] op_sel_hi:[0,0] neg_lo:[0,1]
	v_pk_fma_f32 v[40:41], v[100:101], v[40:41], v[84:85] op_sel_hi:[0,1,1] neg_lo:[1,0,0] neg_hi:[1,0,0]
	v_pk_add_f32 v[84:85], v[44:45], v[96:97]
	v_pk_add_f32 v[44:45], v[44:45], v[96:97] neg_lo:[0,1] neg_hi:[0,1]
	s_nop 0
	v_pk_mul_f32 v[96:97], v[10:11], v[44:45] op_sel:[0,1] op_sel_hi:[0,0] neg_lo:[0,1]
	v_pk_fma_f32 v[44:45], v[10:11], v[44:45], v[96:97] op_sel_hi:[0,1,1] neg_lo:[1,0,0] neg_hi:[1,0,0]
	v_pk_add_f32 v[96:97], v[42:43], v[94:95]
	v_pk_add_f32 v[42:43], v[42:43], v[94:95] neg_lo:[0,1] neg_hi:[0,1]
	s_nop 0
	v_pk_mul_f32 v[94:95], v[100:101], v[42:43] op_sel:[0,1] op_sel_hi:[0,0] neg_lo:[0,1]
	v_pk_fma_f32 v[42:43], v[98:99], v[42:43], v[94:95] op_sel_hi:[0,1,1] neg_lo:[1,0,0] neg_hi:[1,0,0]
	v_pk_add_f32 v[94:95], v[46:47], v[66:67]
	v_pk_add_f32 v[46:47], v[46:47], v[66:67] neg_lo:[0,1] neg_hi:[0,1]
	s_nop 0
	v_pk_mul_f32 v[66:67], v[50:51], v[46:47] op_sel:[0,1] op_sel_hi:[0,0] neg_lo:[0,1]
	v_pk_fma_f32 v[46:47], v[20:21], v[46:47], v[66:67] op_sel_hi:[0,1,1] neg_lo:[1,0,0] neg_hi:[1,0,0]
	v_pk_add_f32 v[66:67], v[48:49], v[68:69]
	v_pk_add_f32 v[48:49], v[48:49], v[68:69] neg_lo:[0,1] neg_hi:[0,1]
	s_nop 0
	v_pk_mul_f32 v[68:69], v[102:103], v[48:49] op_sel:[0,1] op_sel_hi:[0,0] neg_lo:[0,1]
	v_pk_fma_f32 v[48:49], v[92:93], v[48:49], v[68:69] op_sel_hi:[0,1,1] neg_lo:[1,0,0] neg_hi:[1,0,0]
	v_pk_add_f32 v[92:93], v[52:53], v[34:35]
	v_pk_add_f32 v[34:35], v[52:53], v[34:35] neg_lo:[0,1] neg_hi:[0,1]
	v_pk_add_f32 v[68:69], v[104:105], v[82:83]
	v_pk_mul_f32 v[52:53], v[50:51], v[34:35] op_sel:[0,1] op_sel_hi:[0,0] neg_lo:[0,1]
	v_pk_fma_f32 v[34:35], v[20:21], v[34:35], v[52:53] op_sel_hi:[0,1,1]
	v_pk_add_f32 v[52:53], v[70:71], v[88:89]
	v_pk_add_f32 v[70:71], v[70:71], v[88:89] neg_lo:[0,1] neg_hi:[0,1]
	v_pk_add_f32 v[82:83], v[104:105], v[82:83] neg_lo:[0,1] neg_hi:[0,1]
	v_pk_mul_f32 v[88:89], v[10:11], v[70:71] op_sel:[0,1] op_sel_hi:[0,0] neg_lo:[0,1]
	v_pk_fma_f32 v[70:71], v[10:11], v[70:71], v[88:89] op_sel_hi:[0,1,1]
	v_pk_add_f32 v[88:89], v[72:73], v[90:91]
	v_pk_add_f32 v[72:73], v[72:73], v[90:91] neg_lo:[0,1] neg_hi:[0,1]
	s_nop 0
	v_pk_mul_f32 v[90:91], v[20:21], v[72:73] op_sel:[0,1] op_sel_hi:[0,0] neg_lo:[0,1]
	v_pk_fma_f32 v[72:73], v[50:51], v[72:73], v[90:91] op_sel_hi:[0,1,1]
	v_pk_add_f32 v[90:91], v[74:75], v[84:85]
	v_pk_add_f32 v[74:75], v[74:75], v[84:85] neg_lo:[0,1] neg_hi:[0,1]
	s_nop 0
	v_xor_b32_e32 v84, 0x80000000, v75
	v_mov_b32_e32 v85, v74
	v_pk_add_f32 v[74:75], v[76:77], v[96:97]
	v_pk_add_f32 v[76:77], v[76:77], v[96:97] neg_lo:[0,1] neg_hi:[0,1]
	s_nop 0
	v_pk_mul_f32 v[96:97], v[20:21], v[76:77] op_sel:[0,1] op_sel_hi:[0,0] neg_lo:[0,1]
	v_pk_fma_f32 v[76:77], v[50:51], v[76:77], v[96:97] op_sel_hi:[0,1,1] neg_lo:[1,0,0] neg_hi:[1,0,0]
	v_pk_add_f32 v[96:97], v[78:79], v[94:95]
	v_pk_add_f32 v[78:79], v[78:79], v[94:95] neg_lo:[0,1] neg_hi:[0,1]
	s_nop 0
	v_pk_mul_f32 v[94:95], v[10:11], v[78:79] op_sel:[0,1] op_sel_hi:[0,0] neg_lo:[0,1]
	v_pk_fma_f32 v[78:79], v[10:11], v[78:79], v[94:95] op_sel_hi:[0,1,1] neg_lo:[1,0,0] neg_hi:[1,0,0]
	v_pk_add_f32 v[94:95], v[80:81], v[66:67]
	v_pk_add_f32 v[66:67], v[80:81], v[66:67] neg_lo:[0,1] neg_hi:[0,1]
	s_nop 0
	v_pk_mul_f32 v[80:81], v[50:51], v[66:67] op_sel:[0,1] op_sel_hi:[0,0] neg_lo:[0,1]
	v_pk_fma_f32 v[66:67], v[20:21], v[66:67], v[80:81] op_sel_hi:[0,1,1] neg_lo:[1,0,0] neg_hi:[1,0,0]
	v_pk_add_f32 v[80:81], v[68:69], v[90:91]
	v_pk_add_f32 v[68:69], v[68:69], v[90:91] neg_lo:[0,1] neg_hi:[0,1]
	v_pk_add_f32 v[90:91], v[92:93], v[74:75]
	v_pk_add_f32 v[74:75], v[92:93], v[74:75] neg_lo:[0,1] neg_hi:[0,1]
	s_nop 0
	v_pk_mul_f32 v[92:93], v[10:11], v[74:75] op_sel:[0,1] op_sel_hi:[0,0] neg_lo:[0,1]
	v_pk_fma_f32 v[74:75], v[10:11], v[74:75], v[92:93] op_sel_hi:[0,1,1]
	v_pk_add_f32 v[92:93], v[52:53], v[96:97]
	v_pk_add_f32 v[52:53], v[52:53], v[96:97] neg_lo:[0,1] neg_hi:[0,1]
	s_nop 0
	v_xor_b32_e32 v96, 0x80000000, v53
	v_mov_b32_e32 v97, v52
	v_pk_add_f32 v[52:53], v[88:89], v[94:95]
	v_pk_add_f32 v[88:89], v[88:89], v[94:95] neg_lo:[0,1] neg_hi:[0,1]
	s_nop 0
	v_pk_mul_f32 v[94:95], v[10:11], v[88:89] op_sel:[0,1] op_sel_hi:[0,0] neg_lo:[0,1]
	v_pk_fma_f32 v[88:89], v[10:11], v[88:89], v[94:95] op_sel_hi:[0,1,1] neg_lo:[1,0,0] neg_hi:[1,0,0]
	v_pk_add_f32 v[94:95], v[80:81], v[92:93]
	v_pk_add_f32 v[80:81], v[80:81], v[92:93] neg_lo:[0,1] neg_hi:[0,1]
	v_pk_add_f32 v[92:93], v[90:91], v[52:53]
	v_pk_add_f32 v[52:53], v[90:91], v[52:53] neg_lo:[0,1] neg_hi:[0,1]
	s_nop 0
	v_xor_b32_e32 v90, 0x80000000, v53
	v_mov_b32_e32 v91, v52
	v_pk_add_f32 v[52:53], v[94:95], v[92:93]
	v_pk_add_f32 v[92:93], v[94:95], v[92:93] neg_lo:[0,1] neg_hi:[0,1]
	v_pk_add_f32 v[94:95], v[80:81], v[90:91]
	v_pk_add_f32 v[80:81], v[80:81], v[90:91] neg_lo:[0,1] neg_hi:[0,1]
	v_pk_add_f32 v[90:91], v[68:69], v[96:97]
	v_pk_add_f32 v[68:69], v[68:69], v[96:97] neg_lo:[0,1] neg_hi:[0,1]
	v_pk_add_f32 v[96:97], v[74:75], v[88:89]
	v_pk_add_f32 v[74:75], v[74:75], v[88:89] neg_lo:[0,1] neg_hi:[0,1]
	s_nop 0
	v_xor_b32_e32 v88, 0x80000000, v75
	v_mov_b32_e32 v89, v74
	v_pk_add_f32 v[74:75], v[90:91], v[96:97]
	v_pk_add_f32 v[90:91], v[90:91], v[96:97] neg_lo:[0,1] neg_hi:[0,1]
	v_pk_add_f32 v[96:97], v[68:69], v[88:89]
	v_pk_add_f32 v[68:69], v[68:69], v[88:89] neg_lo:[0,1] neg_hi:[0,1]
	v_pk_add_f32 v[88:89], v[82:83], v[84:85]
	v_pk_add_f32 v[82:83], v[82:83], v[84:85] neg_lo:[0,1] neg_hi:[0,1]
	v_pk_add_f32 v[84:85], v[34:35], v[76:77]
	v_pk_add_f32 v[34:35], v[34:35], v[76:77] neg_lo:[0,1] neg_hi:[0,1]
	s_nop 0
	v_pk_mul_f32 v[76:77], v[10:11], v[34:35] op_sel:[0,1] op_sel_hi:[0,0] neg_lo:[0,1]
	v_pk_fma_f32 v[34:35], v[10:11], v[34:35], v[76:77] op_sel_hi:[0,1,1]
	v_pk_add_f32 v[76:77], v[70:71], v[78:79]
	v_pk_add_f32 v[70:71], v[70:71], v[78:79] neg_lo:[0,1] neg_hi:[0,1]
	s_nop 0
	v_xor_b32_e32 v78, 0x80000000, v71
	v_mov_b32_e32 v79, v70
	v_pk_add_f32 v[70:71], v[72:73], v[66:67]
	v_pk_add_f32 v[66:67], v[72:73], v[66:67] neg_lo:[0,1] neg_hi:[0,1]
	s_nop 0
	v_pk_mul_f32 v[72:73], v[10:11], v[66:67] op_sel:[0,1] op_sel_hi:[0,0] neg_lo:[0,1]
	v_pk_fma_f32 v[66:67], v[10:11], v[66:67], v[72:73] op_sel_hi:[0,1,1] neg_lo:[1,0,0] neg_hi:[1,0,0]
	v_pk_add_f32 v[72:73], v[88:89], v[76:77]
	v_pk_add_f32 v[76:77], v[88:89], v[76:77] neg_lo:[0,1] neg_hi:[0,1]
	v_pk_add_f32 v[88:89], v[84:85], v[70:71]
	v_pk_add_f32 v[70:71], v[84:85], v[70:71] neg_lo:[0,1] neg_hi:[0,1]
	s_nop 0
	v_xor_b32_e32 v84, 0x80000000, v71
	v_mov_b32_e32 v85, v70
	v_pk_add_f32 v[70:71], v[72:73], v[88:89]
	v_pk_add_f32 v[72:73], v[72:73], v[88:89] neg_lo:[0,1] neg_hi:[0,1]
	v_pk_add_f32 v[88:89], v[76:77], v[84:85]
	v_pk_add_f32 v[76:77], v[76:77], v[84:85] neg_lo:[0,1] neg_hi:[0,1]
	v_pk_add_f32 v[84:85], v[82:83], v[78:79]
	v_pk_add_f32 v[78:79], v[82:83], v[78:79] neg_lo:[0,1] neg_hi:[0,1]
	v_pk_add_f32 v[82:83], v[34:35], v[66:67]
	v_pk_add_f32 v[34:35], v[34:35], v[66:67] neg_lo:[0,1] neg_hi:[0,1]
	s_nop 0
	v_xor_b32_e32 v66, 0x80000000, v35
	v_mov_b32_e32 v67, v34
	v_pk_add_f32 v[34:35], v[84:85], v[82:83]
	v_pk_add_f32 v[82:83], v[84:85], v[82:83] neg_lo:[0,1] neg_hi:[0,1]
	v_pk_add_f32 v[84:85], v[78:79], v[66:67]
	v_pk_add_f32 v[66:67], v[78:79], v[66:67] neg_lo:[0,1] neg_hi:[0,1]
	v_pk_add_f32 v[78:79], v[16:17], v[86:87]
	v_pk_add_f32 v[16:17], v[16:17], v[86:87] neg_lo:[0,1] neg_hi:[0,1]
	v_pk_add_f32 v[86:87], v[18:19], v[36:37]
	v_pk_add_f32 v[18:19], v[18:19], v[36:37] neg_lo:[0,1] neg_hi:[0,1]
	s_nop 0
	v_pk_mul_f32 v[36:37], v[50:51], v[18:19] op_sel:[0,1] op_sel_hi:[0,0] neg_lo:[0,1]
	v_pk_fma_f32 v[18:19], v[20:21], v[18:19], v[36:37] op_sel_hi:[0,1,1]
	v_pk_add_f32 v[36:37], v[22:23], v[38:39]
	v_pk_add_f32 v[22:23], v[22:23], v[38:39] neg_lo:[0,1] neg_hi:[0,1]
	s_nop 0
	v_pk_mul_f32 v[38:39], v[10:11], v[22:23] op_sel:[0,1] op_sel_hi:[0,0] neg_lo:[0,1]
	v_pk_fma_f32 v[22:23], v[10:11], v[22:23], v[38:39] op_sel_hi:[0,1,1]
	v_pk_add_f32 v[38:39], v[24:25], v[40:41]
	v_pk_add_f32 v[24:25], v[24:25], v[40:41] neg_lo:[0,1] neg_hi:[0,1]
	s_nop 0
	v_pk_mul_f32 v[40:41], v[20:21], v[24:25] op_sel:[0,1] op_sel_hi:[0,0] neg_lo:[0,1]
	v_pk_fma_f32 v[24:25], v[50:51], v[24:25], v[40:41] op_sel_hi:[0,1,1]
	v_pk_add_f32 v[40:41], v[28:29], v[44:45]
	v_pk_add_f32 v[28:29], v[28:29], v[44:45] neg_lo:[0,1] neg_hi:[0,1]
	s_nop 0
	v_xor_b32_e32 v44, 0x80000000, v29
	v_mov_b32_e32 v45, v28
	v_pk_add_f32 v[28:29], v[26:27], v[42:43]
	v_pk_add_f32 v[26:27], v[26:27], v[42:43] neg_lo:[0,1] neg_hi:[0,1]
	s_nop 0
	v_pk_mul_f32 v[42:43], v[20:21], v[26:27] op_sel:[0,1] op_sel_hi:[0,0] neg_lo:[0,1]
	v_pk_fma_f32 v[26:27], v[50:51], v[26:27], v[42:43] op_sel_hi:[0,1,1] neg_lo:[1,0,0] neg_hi:[1,0,0]
	v_pk_add_f32 v[42:43], v[30:31], v[46:47]
	v_pk_add_f32 v[30:31], v[30:31], v[46:47] neg_lo:[0,1] neg_hi:[0,1]
	s_nop 0
	v_pk_mul_f32 v[46:47], v[10:11], v[30:31] op_sel:[0,1] op_sel_hi:[0,0] neg_lo:[0,1]
	v_pk_fma_f32 v[30:31], v[10:11], v[30:31], v[46:47] op_sel_hi:[0,1,1] neg_lo:[1,0,0] neg_hi:[1,0,0]
	v_pk_add_f32 v[46:47], v[32:33], v[48:49]
	v_pk_add_f32 v[32:33], v[32:33], v[48:49] neg_lo:[0,1] neg_hi:[0,1]
	s_nop 0
	v_pk_mul_f32 v[48:49], v[50:51], v[32:33] op_sel:[0,1] op_sel_hi:[0,0] neg_lo:[0,1]
	v_pk_fma_f32 v[20:21], v[20:21], v[32:33], v[48:49] op_sel_hi:[0,1,1] neg_lo:[1,0,0] neg_hi:[1,0,0]
	v_pk_add_f32 v[48:49], v[86:87], v[28:29]
	v_pk_add_f32 v[28:29], v[86:87], v[28:29] neg_lo:[0,1] neg_hi:[0,1]
	v_pk_add_f32 v[32:33], v[78:79], v[40:41]
	v_pk_add_f32 v[40:41], v[78:79], v[40:41] neg_lo:[0,1] neg_hi:[0,1]
	v_pk_mul_f32 v[78:79], v[10:11], v[28:29] op_sel:[0,1] op_sel_hi:[0,0] neg_lo:[0,1]
	v_pk_fma_f32 v[28:29], v[10:11], v[28:29], v[78:79] op_sel_hi:[0,1,1]
	v_pk_add_f32 v[78:79], v[36:37], v[42:43]
	v_pk_add_f32 v[36:37], v[36:37], v[42:43] neg_lo:[0,1] neg_hi:[0,1]
	s_nop 0
	v_xor_b32_e32 v42, 0x80000000, v37
	v_mov_b32_e32 v43, v36
	v_pk_add_f32 v[36:37], v[38:39], v[46:47]
	v_pk_add_f32 v[38:39], v[38:39], v[46:47] neg_lo:[0,1] neg_hi:[0,1]
	s_nop 0
	v_pk_mul_f32 v[46:47], v[10:11], v[38:39] op_sel:[0,1] op_sel_hi:[0,0] neg_lo:[0,1]
	v_pk_fma_f32 v[38:39], v[10:11], v[38:39], v[46:47] op_sel_hi:[0,1,1] neg_lo:[1,0,0] neg_hi:[1,0,0]
	v_pk_add_f32 v[46:47], v[32:33], v[78:79]
	v_pk_add_f32 v[32:33], v[32:33], v[78:79] neg_lo:[0,1] neg_hi:[0,1]
	v_pk_add_f32 v[78:79], v[48:49], v[36:37]
	v_pk_add_f32 v[36:37], v[48:49], v[36:37] neg_lo:[0,1] neg_hi:[0,1]
	s_nop 0
	v_pk_add_f32 v[86:87], v[32:33], v[36:37] op_sel:[0,1] op_sel_hi:[1,0] neg_lo:[0,1]
	v_pk_add_f32 v[32:33], v[32:33], v[36:37] op_sel:[0,1] op_sel_hi:[1,0] neg_hi:[0,1]
	v_pk_add_f32 v[48:49], v[40:41], v[42:43]
	v_pk_add_f32 v[40:41], v[40:41], v[42:43] neg_lo:[0,1] neg_hi:[0,1]
	v_pk_add_f32 v[42:43], v[28:29], v[38:39]
	v_pk_add_f32 v[28:29], v[28:29], v[38:39] neg_lo:[0,1] neg_hi:[0,1]
	v_pk_add_f32 v[36:37], v[46:47], v[78:79] neg_lo:[0,1] neg_hi:[0,1]
	v_xor_b32_e32 v38, 0x80000000, v29
	v_mov_b32_e32 v39, v28
	v_pk_add_f32 v[28:29], v[48:49], v[42:43]
	v_pk_add_f32 v[42:43], v[48:49], v[42:43] neg_lo:[0,1] neg_hi:[0,1]
	v_pk_add_f32 v[48:49], v[40:41], v[38:39]
	v_pk_add_f32 v[38:39], v[40:41], v[38:39] neg_lo:[0,1] neg_hi:[0,1]
	v_pk_add_f32 v[40:41], v[16:17], v[44:45]
	v_pk_add_f32 v[16:17], v[16:17], v[44:45] neg_lo:[0,1] neg_hi:[0,1]
	v_pk_add_f32 v[44:45], v[18:19], v[26:27]
	v_pk_add_f32 v[18:19], v[18:19], v[26:27] neg_lo:[0,1] neg_hi:[0,1]
	s_nop 0
	v_pk_mul_f32 v[26:27], v[10:11], v[18:19] op_sel:[0,1] op_sel_hi:[0,0] neg_lo:[0,1]
	v_pk_fma_f32 v[18:19], v[10:11], v[18:19], v[26:27] op_sel_hi:[0,1,1]
	v_pk_add_f32 v[26:27], v[22:23], v[30:31]
	v_pk_add_f32 v[22:23], v[22:23], v[30:31] neg_lo:[0,1] neg_hi:[0,1]
	s_nop 0
	v_xor_b32_e32 v30, 0x80000000, v23
	v_mov_b32_e32 v31, v22
	v_pk_add_f32 v[22:23], v[24:25], v[20:21]
	v_pk_add_f32 v[20:21], v[24:25], v[20:21] neg_lo:[0,1] neg_hi:[0,1]
	s_nop 0
	v_pk_mul_f32 v[24:25], v[10:11], v[20:21] op_sel:[0,1] op_sel_hi:[0,0] neg_lo:[0,1]
	v_pk_fma_f32 v[20:21], v[10:11], v[20:21], v[24:25] op_sel_hi:[0,1,1] neg_lo:[1,0,0] neg_hi:[1,0,0]
	v_pk_add_f32 v[24:25], v[40:41], v[26:27]
	v_pk_add_f32 v[26:27], v[40:41], v[26:27] neg_lo:[0,1] neg_hi:[0,1]
	v_pk_add_f32 v[40:41], v[44:45], v[22:23]
	v_pk_add_f32 v[22:23], v[44:45], v[22:23] neg_lo:[0,1] neg_hi:[0,1]
	s_nop 0
	v_xor_b32_e32 v44, 0x80000000, v23
	v_mov_b32_e32 v45, v22
	v_pk_add_f32 v[22:23], v[24:25], v[40:41]
	v_pk_add_f32 v[24:25], v[24:25], v[40:41] neg_lo:[0,1] neg_hi:[0,1]
	v_pk_add_f32 v[40:41], v[26:27], v[44:45]
	v_pk_add_f32 v[26:27], v[26:27], v[44:45] neg_lo:[0,1] neg_hi:[0,1]
	v_pk_add_f32 v[44:45], v[16:17], v[30:31]
	v_pk_add_f32 v[16:17], v[16:17], v[30:31] neg_lo:[0,1] neg_hi:[0,1]
	v_pk_add_f32 v[30:31], v[18:19], v[20:21]
	v_pk_add_f32 v[18:19], v[18:19], v[20:21] neg_lo:[0,1] neg_hi:[0,1]
	s_nop 0
	v_xor_b32_e32 v20, 0x80000000, v19
	v_mov_b32_e32 v21, v18
	v_pk_add_f32 v[18:19], v[44:45], v[30:31]
	v_pk_add_f32 v[30:31], v[44:45], v[30:31] neg_lo:[0,1] neg_hi:[0,1]
	v_pk_add_f32 v[44:45], v[16:17], v[20:21]
	v_pk_add_f32 v[16:17], v[16:17], v[20:21] neg_lo:[0,1] neg_hi:[0,1]
	v_pk_add_f32 v[20:21], v[46:47], v[78:79]
	ds_write2_b64 v13, v[52:53], v[20:21] offset1:16
	ds_write2_b64 v15, v[70:71], v[22:23] offset0:32 offset1:48
	ds_write2_b64 v51, v[74:75], v[28:29] offset0:64 offset1:80
	ds_write2_b64 v54, v[34:35], v[18:19] offset0:96 offset1:112
	ds_write2_b64 v55, v[94:95], v[86:87] offset0:128 offset1:144
	ds_write2_b64 v56, v[88:89], v[40:41] offset0:160 offset1:176
	ds_write2_b64 v57, v[96:97], v[48:49] offset0:192 offset1:208
	ds_write2_b64 v58, v[84:85], v[44:45] offset0:224 offset1:240
	ds_write2_b64 v59, v[92:93], v[36:37] offset1:16
	ds_write2_b64 v60, v[72:73], v[24:25] offset0:32 offset1:48
	ds_write2_b64 v61, v[90:91], v[42:43] offset0:64 offset1:80
	ds_write2_b64 v62, v[82:83], v[30:31] offset0:96 offset1:112
	ds_write2_b64 v63, v[80:81], v[32:33] offset0:128 offset1:144
	ds_write2_b64 v64, v[76:77], v[26:27] offset0:160 offset1:176
	ds_write2_b64 v65, v[68:69], v[38:39] offset0:192 offset1:208
	ds_write2_b64 v101, v[66:67], v[16:17] offset0:224 offset1:240
	v_mov_b32_e32 v10, v174
	s_waitcnt lgkmcnt(0)
	s_barrier
	v_mov_b32_e32 v58, v180
	v_mov_b32_e32 v59, v181
	v_lshl_add_u32 v10, v10, 3, 0
	ds_read_b64 v[34:35], v10
	ds_read_b64 v[36:37], v10 offset:4224
	ds_read_b64 v[38:39], v10 offset:8448
	ds_read_b64 v[40:41], v10 offset:12672
	ds_read_b64 v[42:43], v10 offset:16896
	ds_read_b64 v[44:45], v10 offset:21120
	ds_read_b64 v[50:51], v10 offset:25344
	ds_read_b64 v[52:53], v10 offset:29568
	ds_read_b64 v[54:55], v10 offset:33792
	ds_read_b64 v[56:57], v10 offset:38016
	ds_read_b64 v[64:65], v10 offset:42240
	ds_read_b64 v[74:75], v10 offset:46464
	ds_read_b64 v[76:77], v10 offset:50688
	ds_read_b64 v[78:79], v10 offset:54912
	ds_read_b64 v[80:81], v10 offset:59136
	ds_read_b64 v[82:83], v10 offset:63360
	v_add_u32_e32 v13, 0x10800, v10
	v_add_u32_e32 v15, 0x11880, v10
	v_add_u32_e32 v16, 0x12900, v10
	v_add_u32_e32 v17, 0x13980, v10
	ds_read_b64 v[84:85], v13
	ds_read_b64 v[86:87], v15
	ds_read_b64 v[88:89], v16
	ds_read_b64 v[92:93], v17
	v_add_u32_e32 v13, 0x14a00, v10
	v_add_u32_e32 v15, 0x15a80, v10
	v_add_u32_e32 v16, 0x16b00, v10
	v_add_u32_e32 v17, 0x17b80, v10
	ds_read_b64 v[96:97], v13
	ds_read_b64 v[98:99], v15
	ds_read_b64 v[94:95], v16
	ds_read_b64 v[90:91], v17
	v_add_u32_e32 v13, 0x18c00, v10
	v_add_u32_e32 v15, 0x19c80, v10
	v_add_u32_e32 v16, 0x1ad00, v10
	v_add_u32_e32 v17, 0x1bd80, v10
	ds_read_b64 v[72:73], v13
	ds_read_b64 v[70:71], v15
	ds_read_b64 v[68:69], v16
	ds_read_b64 v[66:67], v17
	v_add_u32_e32 v13, 0x1ce00, v10
	v_add_u32_e32 v15, 0x1de80, v10
	v_add_u32_e32 v16, 0x1ef00, v10
	v_add_u32_e32 v10, 0x1ff80, v10
	ds_read_b64 v[62:63], v13
	ds_read_b64 v[60:61], v15
	ds_read_b64 v[100:101], v16
	ds_read_b64 v[102:103], v10
	s_mov_b32 s45, s43
	s_lshl_b64 s[0:1], s[44:45], 2
	v_readlane_b32 s2, v251, 40
	s_add_u32 s0, s2, s0
	v_readlane_b32 s2, v251, 46
	v_mov_b32_e32 v24, v165
	v_mov_b32_e32 v32, v166
	v_mov_b32_e32 v28, v167
	v_mov_b32_e32 v46, v168
	v_mov_b32_e32 v48, v169
	v_mov_b32_e32 v30, v170
	v_mov_b32_e32 v26, v171
	v_mov_b32_e32 v16, v184
	v_mov_b32_e32 v19, v185
	s_addc_u32 s1, s2, s1
	s_waitcnt lgkmcnt(0)
	s_barrier
	global_load_dword v13, v11, s[0:1]
	s_and_b64 s[0:1], s[96:97], exec
	s_movk_i32 s0, 0x800
	s_cselect_b32 s2, 0x400, s0
	v_readlane_b32 s20, v251, 36
	s_add_i32 s4, s2, s20
	s_mul_i32 s0, s4, 0x8200
	v_readlane_b32 s3, v250, 23
	s_mul_hi_i32 s1, s4, 0x8200
	s_add_u32 s0, s3, s0
	v_readlane_b32 s3, v251, 20
	s_addc_u32 s1, s3, s1
	s_lshl_b32 s2, s2, 2
	v_mov_b32_e32 v10, s2
	v_readlane_b32 s2, v251, 50
	v_readlane_b32 s3, v251, 51
	v_readlane_b32 s5, v251, 52
	v_readlane_b32 s6, v251, 18
	v_ashrrev_i32_e32 v15, 31, v14
	v_lshl_add_u64 v[22:23], v[14:15], 2, s[72:73]
	v_cmp_lt_i32_e32 vcc, 0, v14
	global_load_dword v189, v10, s[2:3]
	s_add_i32 s2, s4, 0xc00
	s_ashr_i32 s3, s2, 31
	s_lshl_b64 s[2:3], s[2:3], 2
	s_add_u32 s2, s5, s2
	s_addc_u32 s3, s6, s3
	global_load_dword v191, v11, s[2:3]
	s_add_i32 s2, s4, 0x1800
	s_ashr_i32 s3, s2, 31
	s_lshl_b64 s[2:3], s[2:3], 2
	s_add_u32 s2, s5, s2
	s_addc_u32 s3, s6, s3
	global_load_dword v192, v11, s[2:3]
	v_readlane_b32 s2, v251, 42
	v_readlane_b32 s3, v251, 43
	v_mov_b32_e32 v17, 0
	v_lshl_add_u64 v[20:21], v[14:15], 1, s[0:1]
	v_mov_b32_e32 v18, 0
	v_readlane_b32 s21, v251, 37
	s_nop 0
	global_load_dword v193, v10, s[2:3]
	s_nop 0
	v_lshlrev_b32_e32 v234, 1, v14
	v_lshlrev_b32_e32 v235, 2, v14
	v_add_u32_e32 v235, 0x1000, v235
	global_load_dword v190, v235, s[72:73] offset:-4096
	global_load_ushort v195, v234, s[0:1] offset:-2
	global_load_ushort v196, v234, s[0:1]
	global_load_ushort v197, v234, s[0:1] offset:2
	global_load_dword v198, v235, s[66:67] offset:-4096
	global_load_dword v199, v235, s[72:73] offset:-2048
	global_load_ushort v200, v234, s[0:1] offset:1022
	global_load_ushort v201, v234, s[0:1] offset:1024
	global_load_ushort v202, v234, s[0:1] offset:1026
	global_load_dword v203, v235, s[66:67] offset:-2048
	global_load_dword v204, v235, s[72:73]
	global_load_ushort v205, v234, s[0:1] offset:2046
	global_load_ushort v206, v234, s[0:1] offset:2048
	global_load_ushort v207, v234, s[0:1] offset:2050
	global_load_dword v208, v235, s[66:67]
	global_load_dword v209, v235, s[72:73] offset:2048
	global_load_ushort v210, v234, s[0:1] offset:3070
	global_load_ushort v211, v234, s[0:1] offset:3072
	global_load_ushort v212, v234, s[0:1] offset:3074
	global_load_dword v213, v235, s[66:67] offset:2048
	v_lshlrev_b32_e32 v234, 1, v14
	v_add_u32_e32 v234, 0x1000, v234
	v_lshlrev_b32_e32 v235, 2, v14
	v_add_u32_e32 v235, 0x3000, v235
	global_load_dword v214, v235, s[72:73] offset:-4096
	global_load_ushort v215, v234, s[0:1] offset:-2
	global_load_ushort v216, v234, s[0:1]
	global_load_ushort v217, v234, s[0:1] offset:2
	global_load_dword v218, v235, s[66:67] offset:-4096
	global_load_dword v219, v235, s[72:73] offset:-2048
	global_load_ushort v220, v234, s[0:1] offset:1022
	global_load_ushort v221, v234, s[0:1] offset:1024
	global_load_ushort v222, v234, s[0:1] offset:1026
	global_load_dword v223, v235, s[66:67] offset:-2048
	global_load_dword v224, v235, s[72:73]
	global_load_ushort v225, v234, s[0:1] offset:2046
	global_load_ushort v226, v234, s[0:1] offset:2048
	global_load_ushort v227, v234, s[0:1] offset:2050
	global_load_dword v228, v235, s[66:67]
	global_load_dword v229, v235, s[72:73] offset:2048
	global_load_ushort v230, v234, s[0:1] offset:3070
	global_load_ushort v231, v234, s[0:1] offset:3072
	global_load_ushort v232, v234, s[0:1] offset:3074
	global_load_dword v233, v235, s[66:67] offset:2048
	s_waitcnt vmcnt(20)
	v_mov_b32_e32 v10, v190
	s_and_saveexec_b64 s[2:3], vcc
	s_movk_i32 s10, 0x3fff
	s_cbranch_execz .LBB0_2732
	v_mov_b32_e32 v18, v195
	s_nop 0
	v_lshlrev_b32_e32 v18, 16, v18

.LBB0_2738:
	v_mov_b32_e32 v25, v199
	v_cmp_lt_i32_e32 vcc, s11, v14
	v_mov_b32_e32 v15, 0
	v_mov_b32_e32 v10, 0
	s_and_saveexec_b64 s[4:5], vcc
	s_cbranch_execz .LBB0_2740
	v_mov_b32_e32 v10, v200
	s_nop 0
	v_lshlrev_b32_e32 v10, 16, v10

.LBB0_2746:
	v_add_co_u32_e32 v8, vcc, 0x1000, v22
	v_mov_b32_e32 v15, 0
	s_nop 0
	v_addc_co_u32_e32 v9, vcc, 0, v23, vcc
	v_mov_b32_e32 v120, v204
	v_cmp_lt_i32_e32 vcc, s50, v14
	v_mov_b32_e32 v10, 0
	s_and_saveexec_b64 s[2:3], vcc
	s_cbranch_execz .LBB0_2748
	v_mov_b32_e32 v8, v205
	s_nop 0
	v_lshlrev_b32_e32 v10, 16, v8

.LBB0_2754:
	v_add_co_u32_e32 v74, vcc, 0x1000, v22
	v_mov_b32_e32 v15, 0
	s_nop 0
	v_addc_co_u32_e32 v75, vcc, 0, v23, vcc
	v_mov_b32_e32 v88, v209
	v_cmp_lt_i32_e32 vcc, s51, v14
	v_mov_b32_e32 v10, 0
	s_and_saveexec_b64 s[2:3], vcc
	s_cbranch_execz .LBB0_2756
	v_mov_b32_e32 v10, v210
	s_nop 0
	v_lshlrev_b32_e32 v10, 16, v10

.LBB0_2762:
	v_add_co_u32_e32 v86, vcc, 0x2000, v22
	v_add_u32_e32 v138, 0x800, v14
	s_nop 0
	v_addc_co_u32_e32 v87, vcc, 0, v23, vcc
	v_lshlrev_b32_e32 v234, 1, v14
	v_add_u32_e32 v234, 0x2000, v234
	v_lshlrev_b32_e32 v235, 2, v14
	v_add_u32_e32 v235, 0x5000, v235
	global_load_dword v190, v235, s[72:73] offset:-4096
	global_load_ushort v195, v234, s[0:1] offset:-2
	global_load_ushort v196, v234, s[0:1]
	global_load_ushort v197, v234, s[0:1] offset:2
	global_load_dword v198, v235, s[66:67] offset:-4096
	global_load_dword v199, v235, s[72:73] offset:-2048
	global_load_ushort v200, v234, s[0:1] offset:1022
	global_load_ushort v201, v234, s[0:1] offset:1024
	global_load_ushort v202, v234, s[0:1] offset:1026
	global_load_dword v203, v235, s[66:67] offset:-2048
	global_load_dword v204, v235, s[72:73]
	global_load_ushort v205, v234, s[0:1] offset:2046
	global_load_ushort v206, v234, s[0:1] offset:2048
	global_load_ushort v207, v234, s[0:1] offset:2050
	global_load_dword v208, v235, s[66:67]
	global_load_dword v209, v235, s[72:73] offset:2048
	global_load_ushort v210, v234, s[0:1] offset:3070
	global_load_ushort v211, v234, s[0:1] offset:3072
	global_load_ushort v212, v234, s[0:1] offset:3074
	global_load_dword v213, v235, s[66:67] offset:2048
	s_waitcnt vmcnt(20)
	v_mov_b32_e32 v10, v214
	v_ashrrev_i32_e32 v139, 31, v138
	v_cmp_lt_i32_e32 vcc, s56, v14
	v_mov_b32_e32 v15, 0
	v_mov_b32_e32 v140, 0
	s_and_saveexec_b64 s[2:3], vcc
	s_cbranch_execz .LBB0_2764
	v_mov_b32_e32 v86, v215
	s_nop 0
	v_lshlrev_b32_e32 v140, 16, v86
.LBB0_2764:
	s_or_b64 exec, exec, s[2:3]
	v_add_co_u32_e32 v86, vcc, 0x1000, v20
	s_movk_i32 s2, 0x37ff
	s_nop 0
	v_addc_co_u32_e32 v87, vcc, 0, v21, vcc
	v_mov_b32_e32 v141, v216
	v_cmp_gt_i32_e32 vcc, s2, v14
	s_and_saveexec_b64 s[2:3], vcc
	s_cbranch_execz .LBB0_2766
	s_mov_b64 s[6:7], 0x1000
	v_mov_b32_e32 v15, v217
	s_nop 0
	v_lshlrev_b32_e32 v15, 16, v15

.LBB0_2770:
	v_add_co_u32_e32 v38, vcc, 0x2000, v22
	v_add_u32_e32 v42, 0xa00, v14
	s_nop 0
	v_addc_co_u32_e32 v39, vcc, 0, v23, vcc
	v_mov_b32_e32 v10, v219
	v_ashrrev_i32_e32 v43, 31, v42
	v_cmp_lt_i32_e32 vcc, s57, v14
	v_mov_b32_e32 v15, 0
	v_mov_b32_e32 v44, 0
	s_and_saveexec_b64 s[2:3], vcc
	s_cbranch_execz .LBB0_2772
	v_mov_b32_e32 v38, v220
	s_nop 0
	v_lshlrev_b32_e32 v44, 16, v38
.LBB0_2772:
	s_or_b64 exec, exec, s[2:3]
	v_add_co_u32_e32 v38, vcc, 0x1000, v20
	s_movk_i32 s2, 0x35ff
	s_nop 0
	v_addc_co_u32_e32 v39, vcc, 0, v21, vcc
	v_mov_b32_e32 v45, v221
	v_cmp_gt_i32_e32 vcc, s2, v14
	s_and_saveexec_b64 s[2:3], vcc
	s_cbranch_execz .LBB0_2774
	s_mov_b64 s[6:7], 0x1400
	v_mov_b32_e32 v15, v222
	s_nop 0
	v_lshlrev_b32_e32 v15, 16, v15

.LBB0_2778:
	v_add_co_u32_e32 v42, vcc, 0x3000, v22
	v_add_u32_e32 v116, 0xc00, v14
	s_nop 0
	v_addc_co_u32_e32 v43, vcc, 0, v23, vcc
	v_mov_b32_e32 v10, v224
	v_ashrrev_i32_e32 v117, 31, v116
	v_cmp_lt_i32_e32 vcc, s58, v14
	v_mov_b32_e32 v15, 0
	v_mov_b32_e32 v122, 0
	s_and_saveexec_b64 s[2:3], vcc
	s_cbranch_execz .LBB0_2780
	v_mov_b32_e32 v42, v225
	s_nop 0
	v_lshlrev_b32_e32 v122, 16, v42
.LBB0_2780:
	s_or_b64 exec, exec, s[2:3]
	v_add_co_u32_e32 v42, vcc, 0x1000, v20
	s_movk_i32 s2, 0x33ff
	s_nop 0
	v_addc_co_u32_e32 v43, vcc, 0, v21, vcc
	v_mov_b32_e32 v123, v226
	v_cmp_gt_i32_e32 vcc, s2, v14
	s_and_saveexec_b64 s[2:3], vcc
	s_cbranch_execz .LBB0_2782
	s_mov_b64 s[6:7], 0x1800
	v_mov_b32_e32 v15, v227
	s_nop 0
	v_lshlrev_b32_e32 v15, 16, v15

.LBB0_2786:
	v_add_co_u32_e32 v106, vcc, 0x3000, v22
	v_add_u32_e32 v116, 0xe00, v14
	s_nop 0
	v_addc_co_u32_e32 v107, vcc, 0, v23, vcc
	v_mov_b32_e32 v10, v229
	v_ashrrev_i32_e32 v117, 31, v116
	v_cmp_lt_i32_e32 vcc, s59, v14
	v_mov_b32_e32 v15, 0
	v_mov_b32_e32 v122, 0
	s_and_saveexec_b64 s[2:3], vcc
	s_cbranch_execz .LBB0_2788
	v_mov_b32_e32 v106, v230
	s_nop 0
	v_lshlrev_b32_e32 v122, 16, v106
.LBB0_2788:
	s_or_b64 exec, exec, s[2:3]
	v_add_co_u32_e32 v106, vcc, 0x1000, v20
	s_movk_i32 s2, 0x31ff
	s_nop 0
	v_addc_co_u32_e32 v107, vcc, 0, v21, vcc
	v_mov_b32_e32 v123, v231
	v_cmp_gt_i32_e32 vcc, s2, v14
	s_and_saveexec_b64 s[2:3], vcc
	s_cbranch_execz .LBB0_2790
	s_mov_b64 s[6:7], 0x1c00
	v_mov_b32_e32 v15, v232
	s_nop 0
	v_lshlrev_b32_e32 v15, 16, v15

.LBB0_2794:
	v_add_co_u32_e32 v114, vcc, 0x4000, v22
	v_mov_b32_e32 v15, 0
	s_nop 0
	v_addc_co_u32_e32 v115, vcc, 0, v23, vcc
	v_lshlrev_b32_e32 v234, 1, v14
	v_add_u32_e32 v234, 0x3000, v234
	v_lshlrev_b32_e32 v235, 2, v14
	v_add_u32_e32 v235, 0x7000, v235
	global_load_dword v214, v235, s[72:73] offset:-4096
	global_load_ushort v215, v234, s[0:1] offset:-2
	global_load_ushort v216, v234, s[0:1]
	global_load_ushort v217, v234, s[0:1] offset:2
	global_load_dword v218, v235, s[66:67] offset:-4096
	global_load_dword v219, v235, s[72:73] offset:-2048
	global_load_ushort v220, v234, s[0:1] offset:1022
	global_load_ushort v221, v234, s[0:1] offset:1024
	global_load_ushort v222, v234, s[0:1] offset:1026
	global_load_dword v223, v235, s[66:67] offset:-2048
	global_load_dword v224, v235, s[72:73]
	global_load_ushort v225, v234, s[0:1] offset:2046
	global_load_ushort v226, v234, s[0:1] offset:2048
	global_load_ushort v227, v234, s[0:1] offset:2050
	global_load_dword v228, v235, s[66:67]
	global_load_dword v229, v235, s[72:73] offset:2048
	global_load_ushort v230, v234, s[0:1] offset:3070
	global_load_ushort v231, v234, s[0:1] offset:3072
	global_load_ushort v232, v234, s[0:1] offset:3074
	global_load_dword v233, v235, s[66:67] offset:2048
	s_waitcnt vmcnt(20)
	v_mov_b32_e32 v10, v190
	v_add_u32_e32 v114, 0x1000, v14
	v_ashrrev_i32_e32 v115, 31, v114
	v_cmp_lt_i32_e32 vcc, s60, v14
	v_mov_b32_e32 v116, 0
	s_and_saveexec_b64 s[2:3], vcc
	s_cbranch_execz .LBB0_2796
	v_mov_b32_e32 v116, v195
	s_nop 0
	v_lshlrev_b32_e32 v116, 16, v116

.LBB0_2802:
	v_add_co_u32_e32 v54, vcc, 0x4000, v22
	v_add_u32_e32 v114, 0x1200, v14
	s_nop 0
	v_addc_co_u32_e32 v55, vcc, 0, v23, vcc
	v_mov_b32_e32 v10, v199
	v_ashrrev_i32_e32 v115, 31, v114
	v_cmp_lt_i32_e32 vcc, s62, v14
	v_mov_b32_e32 v15, 0
	v_mov_b32_e32 v116, 0
	s_and_saveexec_b64 s[2:3], vcc
	s_cbranch_execz .LBB0_2804
	v_mov_b32_e32 v54, v200
	s_nop 0
	v_lshlrev_b32_e32 v116, 16, v54
.LBB0_2804:
	s_or_b64 exec, exec, s[2:3]
	v_add_co_u32_e32 v54, vcc, 0x2000, v20
	s_movk_i32 s2, 0x2dff
	s_nop 0
	v_addc_co_u32_e32 v55, vcc, 0, v21, vcc
	v_mov_b32_e32 v117, v201
	v_cmp_gt_i32_e32 vcc, s2, v14
	s_and_saveexec_b64 s[2:3], vcc
	s_cbranch_execz .LBB0_2806
	s_mov_b64 s[6:7], 0x2400
	v_mov_b32_e32 v15, v202
	s_nop 0
	v_lshlrev_b32_e32 v15, 16, v15

.LBB0_2810:
	v_add_co_u32_e32 v66, vcc, 0x5000, v22
	v_mov_b32_e32 v15, 0
	s_nop 0
	v_addc_co_u32_e32 v67, vcc, 0, v23, vcc
	v_mov_b32_e32 v10, v204
	v_add_u32_e32 v66, 0x1400, v14
	v_ashrrev_i32_e32 v67, 31, v66
	v_cmp_lt_i32_e32 vcc, s63, v14
	v_mov_b32_e32 v68, 0
	s_and_saveexec_b64 s[2:3], vcc
	s_cbranch_execz .LBB0_2812
	v_mov_b32_e32 v68, v205
	s_nop 0
	v_lshlrev_b32_e32 v68, 16, v68
.LBB0_2812:
	s_or_b64 exec, exec, s[2:3]
	v_add_co_u32_e32 v70, vcc, 0x2000, v20
	s_movk_i32 s2, 0x2bff
	s_nop 0
	v_addc_co_u32_e32 v71, vcc, 0, v21, vcc
	v_mov_b32_e32 v69, v206
	v_cmp_gt_i32_e32 vcc, s2, v14
	s_and_saveexec_b64 s[2:3], vcc
	s_cbranch_execz .LBB0_2814
	s_mov_b64 s[6:7], 0x2800
	v_mov_b32_e32 v15, v207
	s_nop 0
	v_lshlrev_b32_e32 v15, 16, v15

.LBB0_2818:
	v_add_co_u32_e32 v62, vcc, 0x5000, v22
	v_add_u32_e32 v66, 0x1600, v14
	s_nop 0
	v_addc_co_u32_e32 v63, vcc, 0, v23, vcc
	v_mov_b32_e32 v10, v209
	v_ashrrev_i32_e32 v67, 31, v66
	v_cmp_lt_i32_e32 vcc, s64, v14
	v_mov_b32_e32 v15, 0
	v_mov_b32_e32 v68, 0
	s_and_saveexec_b64 s[2:3], vcc
	s_cbranch_execz .LBB0_2820
	v_mov_b32_e32 v62, v210
	s_nop 0
	v_lshlrev_b32_e32 v68, 16, v62
.LBB0_2820:
	s_or_b64 exec, exec, s[2:3]
	v_add_co_u32_e32 v62, vcc, 0x2000, v20
	s_movk_i32 s2, 0x29ff
	s_nop 0
	v_addc_co_u32_e32 v63, vcc, 0, v21, vcc
	v_mov_b32_e32 v69, v211
	v_cmp_gt_i32_e32 vcc, s2, v14
	s_and_saveexec_b64 s[2:3], vcc
	s_cbranch_execz .LBB0_2822
	s_mov_b64 s[6:7], 0x2c00
	v_mov_b32_e32 v15, v212
	s_nop 0
	v_lshlrev_b32_e32 v15, 16, v15

.LBB0_2826:
	v_add_co_u32_e32 v66, vcc, 0x6000, v22
	v_add_u32_e32 v70, 0x1800, v14
	s_nop 0
	v_addc_co_u32_e32 v67, vcc, 0, v23, vcc
	v_lshlrev_b32_e32 v234, 1, v14
	v_add_u32_e32 v234, 0x4000, v234
	v_lshlrev_b32_e32 v235, 2, v14
	v_add_u32_e32 v235, 0x9000, v235
	global_load_dword v190, v235, s[72:73] offset:-4096
	global_load_ushort v195, v234, s[0:1] offset:-2
	global_load_ushort v196, v234, s[0:1]
	global_load_ushort v197, v234, s[0:1] offset:2
	global_load_dword v198, v235, s[66:67] offset:-4096
	global_load_dword v199, v235, s[72:73] offset:-2048
	global_load_ushort v200, v234, s[0:1] offset:1022
	global_load_ushort v201, v234, s[0:1] offset:1024
	global_load_ushort v202, v234, s[0:1] offset:1026
	global_load_dword v203, v235, s[66:67] offset:-2048
	global_load_dword v204, v235, s[72:73]
	global_load_ushort v205, v234, s[0:1] offset:2046
	global_load_ushort v206, v234, s[0:1] offset:2048
	global_load_ushort v207, v234, s[0:1] offset:2050
	global_load_dword v208, v235, s[66:67]
	global_load_dword v209, v235, s[72:73] offset:2048
	global_load_ushort v210, v234, s[0:1] offset:3070
	global_load_ushort v211, v234, s[0:1] offset:3072
	global_load_ushort v212, v234, s[0:1] offset:3074
	global_load_dword v213, v235, s[66:67] offset:2048
	s_waitcnt vmcnt(20)
	v_mov_b32_e32 v10, v214
	v_ashrrev_i32_e32 v71, 31, v70
	v_cmp_lt_i32_e32 vcc, s65, v14
	v_mov_b32_e32 v15, 0
	v_mov_b32_e32 v72, 0
	s_and_saveexec_b64 s[2:3], vcc
	s_cbranch_execz .LBB0_2828
	v_mov_b32_e32 v66, v215
	s_nop 0
	v_lshlrev_b32_e32 v72, 16, v66
.LBB0_2828:
	s_or_b64 exec, exec, s[2:3]
	v_add_co_u32_e32 v66, vcc, 0x3000, v20
	s_movk_i32 s2, 0x27ff
	s_nop 0
	v_addc_co_u32_e32 v67, vcc, 0, v21, vcc
	v_mov_b32_e32 v73, v216
	v_cmp_gt_i32_e32 vcc, s2, v14
	s_and_saveexec_b64 s[2:3], vcc
	s_cbranch_execz .LBB0_2830
	s_mov_b64 s[6:7], 0x3000
	v_mov_b32_e32 v15, v217
	s_nop 0
	v_lshlrev_b32_e32 v15, 16, v15

.LBB0_2834:
	v_add_co_u32_e32 v70, vcc, 0x6000, v22
	v_add_u32_e32 v74, 0x1a00, v14
	s_nop 0
	v_addc_co_u32_e32 v71, vcc, 0, v23, vcc
	v_mov_b32_e32 v10, v219
	s_movk_i32 s2, 0xe600
	v_ashrrev_i32_e32 v75, 31, v74
	v_cmp_lt_i32_e32 vcc, s2, v14
	v_mov_b32_e32 v15, 0
	v_mov_b32_e32 v76, 0
	s_and_saveexec_b64 s[2:3], vcc
	s_cbranch_execz .LBB0_2836
	v_mov_b32_e32 v70, v220
	s_nop 0
	v_lshlrev_b32_e32 v76, 16, v70
.LBB0_2836:
	s_or_b64 exec, exec, s[2:3]
	v_add_co_u32_e32 v70, vcc, 0x3000, v20
	s_movk_i32 s2, 0x25ff
	s_nop 0
	v_addc_co_u32_e32 v71, vcc, 0, v21, vcc
	v_mov_b32_e32 v77, v221
	v_cmp_gt_i32_e32 vcc, s2, v14
	s_and_saveexec_b64 s[2:3], vcc
	s_cbranch_execz .LBB0_2838
	s_mov_b64 s[6:7], 0x3400
	v_mov_b32_e32 v15, v222
	s_nop 0
	v_lshlrev_b32_e32 v15, 16, v15

.LBB0_2842:
	v_add_co_u32_e32 v74, vcc, 0x7000, v22
	v_add_u32_e32 v78, 0x1c00, v14
	s_nop 0
	v_addc_co_u32_e32 v75, vcc, 0, v23, vcc
	v_mov_b32_e32 v10, v224
	s_movk_i32 s2, 0xe400
	v_ashrrev_i32_e32 v79, 31, v78
	v_cmp_lt_i32_e32 vcc, s2, v14
	v_mov_b32_e32 v15, 0
	v_mov_b32_e32 v80, 0
	s_and_saveexec_b64 s[2:3], vcc
	s_cbranch_execz .LBB0_2844
	v_mov_b32_e32 v74, v225
	s_nop 0
	v_lshlrev_b32_e32 v80, 16, v74
.LBB0_2844:
	s_or_b64 exec, exec, s[2:3]
	v_add_co_u32_e32 v74, vcc, 0x3000, v20
	s_movk_i32 s2, 0x23ff
	s_nop 0
	v_addc_co_u32_e32 v75, vcc, 0, v21, vcc
	v_mov_b32_e32 v81, v226
	v_cmp_gt_i32_e32 vcc, s2, v14
	s_and_saveexec_b64 s[2:3], vcc
	s_cbranch_execz .LBB0_2846
	s_mov_b64 s[6:7], 0x3800
	v_mov_b32_e32 v15, v227
	s_nop 0
	v_lshlrev_b32_e32 v15, 16, v15

.LBB0_2850:
	v_add_co_u32_e32 v78, vcc, 0x7000, v22
	v_add_u32_e32 v82, 0x1e00, v14
	s_nop 0
	v_addc_co_u32_e32 v79, vcc, 0, v23, vcc
	v_mov_b32_e32 v10, v229
	s_movk_i32 s2, 0xe200
	v_ashrrev_i32_e32 v83, 31, v82
	v_cmp_lt_i32_e32 vcc, s2, v14
	v_mov_b32_e32 v15, 0
	v_mov_b32_e32 v84, 0
	s_and_saveexec_b64 s[2:3], vcc
	s_cbranch_execz .LBB0_2852
	v_mov_b32_e32 v78, v230
	s_nop 0
	v_lshlrev_b32_e32 v84, 16, v78
.LBB0_2852:
	s_or_b64 exec, exec, s[2:3]
	v_add_co_u32_e32 v78, vcc, 0x3000, v20
	s_movk_i32 s2, 0x21ff
	s_nop 0
	v_addc_co_u32_e32 v79, vcc, 0, v21, vcc
	v_mov_b32_e32 v85, v231
	v_cmp_gt_i32_e32 vcc, s2, v14
	s_and_saveexec_b64 s[2:3], vcc
	s_cbranch_execz .LBB0_2854
	s_mov_b64 s[6:7], 0x3c00
	v_mov_b32_e32 v15, v232
	s_nop 0
	v_lshlrev_b32_e32 v15, 16, v15

.LBB0_2858:
	v_add_co_u32_e32 v82, vcc, 0x8000, v22
	s_movk_i32 s2, 0xe000
	s_nop 0
	v_addc_co_u32_e32 v83, vcc, 0, v23, vcc
	v_lshlrev_b32_e32 v234, 1, v14
	v_add_u32_e32 v234, 0x5000, v234
	v_lshlrev_b32_e32 v235, 2, v14
	v_add_u32_e32 v235, 0xb000, v235
	global_load_dword v214, v235, s[72:73] offset:-4096
	global_load_ushort v215, v234, s[0:1] offset:-2
	global_load_ushort v216, v234, s[0:1]
	global_load_ushort v217, v234, s[0:1] offset:2
	global_load_dword v218, v235, s[66:67] offset:-4096
	global_load_dword v219, v235, s[72:73] offset:-2048
	global_load_ushort v220, v234, s[0:1] offset:1022
	global_load_ushort v221, v234, s[0:1] offset:1024
	global_load_ushort v222, v234, s[0:1] offset:1026
	global_load_dword v223, v235, s[66:67] offset:-2048
	global_load_dword v224, v235, s[72:73]
	global_load_ushort v225, v234, s[0:1] offset:2046
	global_load_ushort v226, v234, s[0:1] offset:2048
	global_load_ushort v227, v234, s[0:1] offset:2050
	global_load_dword v228, v235, s[66:67]
	global_load_dword v229, v235, s[72:73] offset:2048
	global_load_ushort v230, v234, s[0:1] offset:3070
	global_load_ushort v231, v234, s[0:1] offset:3072
	global_load_ushort v232, v234, s[0:1] offset:3074
	global_load_dword v233, v235, s[66:67] offset:2048
	s_waitcnt vmcnt(20)
	v_mov_b32_e32 v10, v190
	v_add_u32_e32 v82, 0x2000, v14
	v_ashrrev_i32_e32 v83, 31, v82
	v_cmp_lt_i32_e32 vcc, s2, v14
	v_mov_b32_e32 v15, 0
	v_mov_b32_e32 v84, 0
	s_and_saveexec_b64 s[2:3], vcc
	s_cbranch_execz .LBB0_2860
	v_mov_b32_e32 v84, v195
	s_nop 0
	v_lshlrev_b32_e32 v84, 16, v84

.LBB0_2866:
	v_add_co_u32_e32 v4, vcc, 0x8000, v22
	s_movk_i32 s2, 0xde00
	s_nop 0
	v_addc_co_u32_e32 v5, vcc, 0, v23, vcc
	v_mov_b32_e32 v6, v199
	v_add_u32_e32 v4, 0x2200, v14
	v_ashrrev_i32_e32 v5, 31, v4
	v_cmp_lt_i32_e32 vcc, s2, v14
	v_mov_b32_e32 v7, 0
	v_mov_b32_e32 v10, 0
	s_and_saveexec_b64 s[2:3], vcc
	s_cbranch_execz .LBB0_2868
	v_mov_b32_e32 v10, v200
	s_nop 0
	v_lshlrev_b32_e32 v10, 16, v10

.LBB0_2874:
	v_add_co_u32_e32 v4, vcc, 0x9000, v22
	s_movk_i32 s2, 0xdc00
	s_nop 0
	v_addc_co_u32_e32 v5, vcc, 0, v23, vcc
	v_mov_b32_e32 v6, v204
	v_add_u32_e32 v4, 0x2400, v14
	v_ashrrev_i32_e32 v5, 31, v4
	v_cmp_lt_i32_e32 vcc, s2, v14
	v_mov_b32_e32 v7, 0
	v_mov_b32_e32 v10, 0
	s_and_saveexec_b64 s[2:3], vcc
	s_cbranch_execz .LBB0_2876
	v_mov_b32_e32 v10, v205
	s_nop 0
	v_lshlrev_b32_e32 v10, 16, v10
.LBB0_2876:
	s_or_b64 exec, exec, s[2:3]
	v_add_co_u32_e32 v26, vcc, 0x4000, v20
	s_movk_i32 s2, 0x1bff
	s_nop 0
	v_addc_co_u32_e32 v27, vcc, 0, v21, vcc
	v_mov_b32_e32 v15, v206
	v_cmp_gt_i32_e32 vcc, s2, v14
	s_and_saveexec_b64 s[2:3], vcc
	s_cbranch_execz .LBB0_2878
	s_mov_b64 s[6:7], 0x4800
	v_mov_b32_e32 v7, v207
	s_nop 0
	v_lshlrev_b32_e32 v7, 16, v7

.LBB0_2882:
	v_add_co_u32_e32 v4, vcc, 0x9000, v22
	s_movk_i32 s2, 0xda00
	s_nop 0
	v_addc_co_u32_e32 v5, vcc, 0, v23, vcc
	v_mov_b32_e32 v6, v209
	v_add_u32_e32 v4, 0x2600, v14
	v_ashrrev_i32_e32 v5, 31, v4
	v_cmp_lt_i32_e32 vcc, s2, v14
	v_mov_b32_e32 v7, 0
	v_mov_b32_e32 v8, 0
	s_and_saveexec_b64 s[2:3], vcc
	s_cbranch_execz .LBB0_2884
	v_mov_b32_e32 v8, v210
	s_nop 0
	v_lshlrev_b32_e32 v8, 16, v8
.LBB0_2884:
	s_or_b64 exec, exec, s[2:3]
	v_add_co_u32_e32 v24, vcc, 0x4000, v20
	s_movk_i32 s2, 0x19ff
	s_nop 0
	v_addc_co_u32_e32 v25, vcc, 0, v21, vcc
	v_mov_b32_e32 v9, v211
	v_cmp_gt_i32_e32 vcc, s2, v14
	s_and_saveexec_b64 s[2:3], vcc
	s_cbranch_execz .LBB0_2886
	s_mov_b64 s[6:7], 0x4c00
	v_mov_b32_e32 v7, v212
	s_nop 0
	v_lshlrev_b32_e32 v7, 16, v7

.LBB0_2890:
	v_add_co_u32_e32 v4, vcc, 0xa000, v22
	s_movk_i32 s2, 0xd800
	s_nop 0
	v_addc_co_u32_e32 v5, vcc, 0, v23, vcc
	v_lshlrev_b32_e32 v234, 1, v14
	v_add_u32_e32 v234, 0x6000, v234
	v_lshlrev_b32_e32 v235, 2, v14
	v_add_u32_e32 v235, 0xd000, v235
	global_load_dword v190, v235, s[72:73] offset:-4096
	global_load_ushort v195, v234, s[0:1] offset:-2
	global_load_ushort v196, v234, s[0:1]
	global_load_ushort v197, v234, s[0:1] offset:2
	global_load_dword v198, v235, s[66:67] offset:-4096
	global_load_dword v199, v235, s[72:73] offset:-2048
	global_load_ushort v200, v234, s[0:1] offset:1022
	global_load_ushort v201, v234, s[0:1] offset:1024
	global_load_ushort v202, v234, s[0:1] offset:1026
	global_load_dword v203, v235, s[66:67] offset:-2048
	global_load_dword v204, v235, s[72:73]
	global_load_ushort v205, v234, s[0:1] offset:2046
	global_load_ushort v206, v234, s[0:1] offset:2048
	global_load_ushort v207, v234, s[0:1] offset:2050
	global_load_dword v208, v235, s[66:67]
	global_load_dword v209, v235, s[72:73] offset:2048
	global_load_ushort v210, v234, s[0:1] offset:3070
	global_load_ushort v211, v234, s[0:1] offset:3072
	global_load_ushort v212, v234, s[0:1] offset:3074
	global_load_dword v213, v235, s[66:67] offset:2048
	s_waitcnt vmcnt(20)
	v_mov_b32_e32 v6, v214
	v_add_u32_e32 v4, 0x2800, v14
	v_ashrrev_i32_e32 v5, 31, v4
	v_cmp_lt_i32_e32 vcc, s2, v14
	v_mov_b32_e32 v7, 0
	v_mov_b32_e32 v8, 0
	s_and_saveexec_b64 s[2:3], vcc
	s_cbranch_execz .LBB0_2892
	v_mov_b32_e32 v8, v215
	s_nop 0
	v_lshlrev_b32_e32 v8, 16, v8
.LBB0_2892:
	s_or_b64 exec, exec, s[2:3]
	v_add_co_u32_e32 v24, vcc, 0x5000, v20
	s_movk_i32 s2, 0x17ff
	s_nop 0
	v_addc_co_u32_e32 v25, vcc, 0, v21, vcc
	v_mov_b32_e32 v9, v216
	v_cmp_gt_i32_e32 vcc, s2, v14
	s_and_saveexec_b64 s[2:3], vcc
	s_cbranch_execz .LBB0_2894
	s_mov_b64 s[6:7], 0x5000
	v_mov_b32_e32 v7, v217
	s_nop 0
	v_lshlrev_b32_e32 v7, 16, v7

.LBB0_2898:
	v_add_co_u32_e32 v4, vcc, 0xa000, v22
	s_movk_i32 s2, 0xd600
	s_nop 0
	v_addc_co_u32_e32 v5, vcc, 0, v23, vcc
	v_mov_b32_e32 v6, v219
	v_add_u32_e32 v4, 0x2a00, v14
	v_ashrrev_i32_e32 v5, 31, v4
	v_cmp_lt_i32_e32 vcc, s2, v14
	v_mov_b32_e32 v7, 0
	v_mov_b32_e32 v8, 0
	s_and_saveexec_b64 s[2:3], vcc
	s_cbranch_execz .LBB0_2900
	v_mov_b32_e32 v8, v220
	s_nop 0
	v_lshlrev_b32_e32 v8, 16, v8
.LBB0_2900:
	s_or_b64 exec, exec, s[2:3]
	v_add_co_u32_e32 v24, vcc, 0x5000, v20
	s_movk_i32 s2, 0x15ff
	s_nop 0
	v_addc_co_u32_e32 v25, vcc, 0, v21, vcc
	v_mov_b32_e32 v9, v221
	v_cmp_gt_i32_e32 vcc, s2, v14
	s_and_saveexec_b64 s[2:3], vcc
	s_cbranch_execz .LBB0_2902
	s_mov_b64 s[6:7], 0x5400
	v_mov_b32_e32 v7, v222
	s_nop 0
	v_lshlrev_b32_e32 v7, 16, v7

.LBB0_2906:
	v_add_co_u32_e32 v4, vcc, 0xb000, v22
	s_movk_i32 s2, 0xd400
	s_nop 0
	v_addc_co_u32_e32 v5, vcc, 0, v23, vcc
	v_mov_b32_e32 v6, v224
	v_add_u32_e32 v4, 0x2c00, v14
	v_ashrrev_i32_e32 v5, 31, v4
	v_cmp_lt_i32_e32 vcc, s2, v14
	v_mov_b32_e32 v7, 0
	v_mov_b32_e32 v8, 0
	s_and_saveexec_b64 s[2:3], vcc
	s_cbranch_execz .LBB0_2908
	v_mov_b32_e32 v8, v225
	s_nop 0
	v_lshlrev_b32_e32 v8, 16, v8
.LBB0_2908:
	s_or_b64 exec, exec, s[2:3]
	v_add_co_u32_e32 v24, vcc, 0x5000, v20
	s_movk_i32 s2, 0x13ff
	s_nop 0
	v_addc_co_u32_e32 v25, vcc, 0, v21, vcc
	v_mov_b32_e32 v9, v226
	v_cmp_gt_i32_e32 vcc, s2, v14
	s_and_saveexec_b64 s[2:3], vcc
	s_cbranch_execz .LBB0_2910
	s_mov_b64 s[6:7], 0x5800
	v_mov_b32_e32 v7, v227
	s_nop 0
	v_lshlrev_b32_e32 v7, 16, v7

.LBB0_2914:
	v_add_co_u32_e32 v4, vcc, 0xb000, v22
	s_movk_i32 s2, 0xd200
	s_nop 0
	v_addc_co_u32_e32 v5, vcc, 0, v23, vcc
	v_mov_b32_e32 v6, v229
	v_add_u32_e32 v4, 0x2e00, v14
	v_ashrrev_i32_e32 v5, 31, v4
	v_cmp_lt_i32_e32 vcc, s2, v14
	v_mov_b32_e32 v7, 0
	v_mov_b32_e32 v8, 0
	s_and_saveexec_b64 s[2:3], vcc
	s_cbranch_execz .LBB0_2916
	v_mov_b32_e32 v8, v230
	s_nop 0
	v_lshlrev_b32_e32 v8, 16, v8
.LBB0_2916:
	s_or_b64 exec, exec, s[2:3]
	v_add_co_u32_e32 v24, vcc, 0x5000, v20
	s_movk_i32 s2, 0x11ff
	s_nop 0
	v_addc_co_u32_e32 v25, vcc, 0, v21, vcc
	v_mov_b32_e32 v9, v231
	v_cmp_gt_i32_e32 vcc, s2, v14
	s_and_saveexec_b64 s[2:3], vcc
	s_cbranch_execz .LBB0_2918
	s_mov_b64 s[6:7], 0x5c00
	v_mov_b32_e32 v7, v232
	s_nop 0
	v_lshlrev_b32_e32 v7, 16, v7

.LBB0_2922:
	v_add_co_u32_e32 v4, vcc, 0xc000, v22
	s_movk_i32 s2, 0xd000
	s_nop 0
	v_addc_co_u32_e32 v5, vcc, 0, v23, vcc
	v_lshlrev_b32_e32 v234, 1, v14
	v_add_u32_e32 v234, 0x7000, v234
	v_lshlrev_b32_e32 v235, 2, v14
	v_add_u32_e32 v235, 0xf000, v235
	global_load_dword v214, v235, s[72:73] offset:-4096
	global_load_ushort v215, v234, s[0:1] offset:-2
	global_load_ushort v216, v234, s[0:1]
	global_load_ushort v217, v234, s[0:1] offset:2
	global_load_dword v218, v235, s[66:67] offset:-4096
	global_load_dword v219, v235, s[72:73] offset:-2048
	global_load_ushort v220, v234, s[0:1] offset:1022
	global_load_ushort v221, v234, s[0:1] offset:1024
	global_load_ushort v222, v234, s[0:1] offset:1026
	global_load_dword v223, v235, s[66:67] offset:-2048
	global_load_dword v224, v235, s[72:73]
	global_load_ushort v225, v234, s[0:1] offset:2046
	global_load_ushort v226, v234, s[0:1] offset:2048
	global_load_ushort v227, v234, s[0:1] offset:2050
	global_load_dword v228, v235, s[66:67]
	global_load_dword v229, v235, s[72:73] offset:2048
	global_load_ushort v230, v234, s[0:1] offset:3070
	global_load_ushort v231, v234, s[0:1] offset:3072
	global_load_ushort v232, v234, s[0:1] offset:3074
	global_load_dword v233, v235, s[66:67] offset:2048
	s_waitcnt vmcnt(20)
	v_mov_b32_e32 v6, v190
	v_add_u32_e32 v4, 0x3000, v14
	v_ashrrev_i32_e32 v5, 31, v4
	v_cmp_lt_i32_e32 vcc, s2, v14
	v_mov_b32_e32 v7, 0
	v_mov_b32_e32 v8, 0
	s_and_saveexec_b64 s[2:3], vcc
	s_cbranch_execz .LBB0_2924
	v_mov_b32_e32 v8, v195
	s_nop 0
	v_lshlrev_b32_e32 v8, 16, v8
.LBB0_2924:
	s_or_b64 exec, exec, s[2:3]
	v_add_co_u32_e32 v24, vcc, 0x6000, v20
	s_movk_i32 s2, 0xfff
	s_nop 0
	v_addc_co_u32_e32 v25, vcc, 0, v21, vcc
	v_mov_b32_e32 v9, v196
	v_cmp_gt_i32_e32 vcc, s2, v14
	s_and_saveexec_b64 s[2:3], vcc
	s_cbranch_execz .LBB0_2926
	s_mov_b64 s[6:7], 0x6000
	v_mov_b32_e32 v7, v197
	s_nop 0
	v_lshlrev_b32_e32 v7, 16, v7

.LBB0_2930:
	v_add_co_u32_e32 v4, vcc, 0xc000, v22
	s_movk_i32 s2, 0xce00
	s_nop 0
	v_addc_co_u32_e32 v5, vcc, 0, v23, vcc
	v_mov_b32_e32 v6, v199
	v_add_u32_e32 v4, 0x3200, v14
	v_ashrrev_i32_e32 v5, 31, v4
	v_cmp_lt_i32_e32 vcc, s2, v14
	v_mov_b32_e32 v7, 0
	v_mov_b32_e32 v8, 0
	s_and_saveexec_b64 s[2:3], vcc
	s_cbranch_execz .LBB0_2932
	v_mov_b32_e32 v8, v200
	s_nop 0
	v_lshlrev_b32_e32 v8, 16, v8
.LBB0_2932:
	s_or_b64 exec, exec, s[2:3]
	v_add_co_u32_e32 v24, vcc, 0x6000, v20
	s_movk_i32 s2, 0xdff
	s_nop 0
	v_addc_co_u32_e32 v25, vcc, 0, v21, vcc
	v_mov_b32_e32 v9, v201
	v_cmp_gt_i32_e32 vcc, s2, v14
	s_and_saveexec_b64 s[2:3], vcc
	s_cbranch_execz .LBB0_2934
	s_mov_b64 s[6:7], 0x6400
	v_mov_b32_e32 v7, v202
	s_nop 0
	v_lshlrev_b32_e32 v7, 16, v7

.LBB0_2938:
	v_add_co_u32_e32 v4, vcc, 0xd000, v22
	s_movk_i32 s2, 0xcc00
	s_nop 0
	v_addc_co_u32_e32 v5, vcc, 0, v23, vcc
	v_mov_b32_e32 v6, v204
	v_add_u32_e32 v4, 0x3400, v14
	v_ashrrev_i32_e32 v5, 31, v4
	v_cmp_lt_i32_e32 vcc, s2, v14
	v_mov_b32_e32 v7, 0
	v_mov_b32_e32 v8, 0
	s_and_saveexec_b64 s[2:3], vcc
	s_cbranch_execz .LBB0_2940
	v_mov_b32_e32 v8, v205
	s_nop 0
	v_lshlrev_b32_e32 v8, 16, v8
.LBB0_2940:
	s_or_b64 exec, exec, s[2:3]
	v_add_co_u32_e32 v24, vcc, 0x6000, v20
	s_movk_i32 s2, 0xbff
	s_nop 0
	v_addc_co_u32_e32 v25, vcc, 0, v21, vcc
	v_mov_b32_e32 v9, v206
	v_cmp_gt_i32_e32 vcc, s2, v14
	s_and_saveexec_b64 s[2:3], vcc
	s_cbranch_execz .LBB0_2942
	s_mov_b64 s[6:7], 0x6800
	v_mov_b32_e32 v7, v207
	s_nop 0
	v_lshlrev_b32_e32 v7, 16, v7

.LBB0_2946:
	v_add_co_u32_e32 v4, vcc, 0xd000, v22
	s_movk_i32 s2, 0xca00
	s_nop 0
	v_addc_co_u32_e32 v5, vcc, 0, v23, vcc
	v_mov_b32_e32 v6, v209
	v_add_u32_e32 v4, 0x3600, v14
	v_ashrrev_i32_e32 v5, 31, v4
	v_cmp_lt_i32_e32 vcc, s2, v14
	v_mov_b32_e32 v7, 0
	v_mov_b32_e32 v8, 0
	s_and_saveexec_b64 s[2:3], vcc
	s_cbranch_execz .LBB0_2948
	v_mov_b32_e32 v8, v210
	s_nop 0
	v_lshlrev_b32_e32 v8, 16, v8
.LBB0_2948:
	s_or_b64 exec, exec, s[2:3]
	v_add_co_u32_e32 v24, vcc, 0x6000, v20
	s_movk_i32 s2, 0x9ff
	s_nop 0
	v_addc_co_u32_e32 v25, vcc, 0, v21, vcc
	v_mov_b32_e32 v9, v211
	v_cmp_gt_i32_e32 vcc, s2, v14
	s_and_saveexec_b64 s[2:3], vcc
	s_cbranch_execz .LBB0_2950
	s_mov_b64 s[6:7], 0x6c00
	v_mov_b32_e32 v7, v212
	s_nop 0
	v_lshlrev_b32_e32 v7, 16, v7

.LBB0_2954:
	v_add_co_u32_e32 v4, vcc, 0xe000, v22
	s_movk_i32 s2, 0xc800
	s_nop 0
	v_addc_co_u32_e32 v5, vcc, 0, v23, vcc
	s_waitcnt vmcnt(0)
	v_mov_b32_e32 v6, v214
	v_add_u32_e32 v4, 0x3800, v14
	v_ashrrev_i32_e32 v5, 31, v4
	v_cmp_lt_i32_e32 vcc, s2, v14
	v_mov_b32_e32 v7, 0
	v_mov_b32_e32 v8, 0
	s_and_saveexec_b64 s[2:3], vcc
	s_cbranch_execz .LBB0_2956
	v_mov_b32_e32 v8, v215
	s_nop 0
	v_lshlrev_b32_e32 v8, 16, v8
.LBB0_2956:
	s_or_b64 exec, exec, s[2:3]
	v_add_co_u32_e32 v24, vcc, 0x7000, v20
	s_movk_i32 s2, 0x7ff
	s_nop 0
	v_addc_co_u32_e32 v25, vcc, 0, v21, vcc
	v_mov_b32_e32 v9, v216
	v_cmp_gt_i32_e32 vcc, s2, v14
	s_and_saveexec_b64 s[2:3], vcc
	s_cbranch_execz .LBB0_2958
	s_mov_b64 s[6:7], 0x7000
	v_mov_b32_e32 v7, v217
	s_nop 0
	v_lshlrev_b32_e32 v7, 16, v7

.LBB0_2962:
	v_add_co_u32_e32 v4, vcc, 0xe000, v22
	s_movk_i32 s2, 0xc600
	s_nop 0
	v_addc_co_u32_e32 v5, vcc, 0, v23, vcc
	v_mov_b32_e32 v6, v219
	v_add_u32_e32 v4, 0x3a00, v14
	v_ashrrev_i32_e32 v5, 31, v4
	v_cmp_lt_i32_e32 vcc, s2, v14
	v_mov_b32_e32 v7, 0
	v_mov_b32_e32 v8, 0
	s_and_saveexec_b64 s[2:3], vcc
	s_cbranch_execz .LBB0_2964
	v_mov_b32_e32 v8, v220
	s_nop 0
	v_lshlrev_b32_e32 v8, 16, v8
.LBB0_2964:
	s_or_b64 exec, exec, s[2:3]
	v_add_co_u32_e32 v24, vcc, 0x7000, v20
	s_movk_i32 s2, 0x5ff
	s_nop 0
	v_addc_co_u32_e32 v25, vcc, 0, v21, vcc
	v_mov_b32_e32 v9, v221
	v_cmp_gt_i32_e32 vcc, s2, v14
	s_and_saveexec_b64 s[2:3], vcc
	s_cbranch_execz .LBB0_2966
	s_mov_b64 s[6:7], 0x7400
	v_mov_b32_e32 v7, v222
	s_nop 0
	v_lshlrev_b32_e32 v7, 16, v7

.LBB0_2970:
	v_add_co_u32_e32 v4, vcc, 0xf000, v22
	s_movk_i32 s2, 0xc400
	s_nop 0
	v_addc_co_u32_e32 v5, vcc, 0, v23, vcc
	v_mov_b32_e32 v6, v224
	v_add_u32_e32 v4, 0x3c00, v14
	v_ashrrev_i32_e32 v5, 31, v4
	v_cmp_lt_i32_e32 vcc, s2, v14
	v_mov_b32_e32 v7, 0
	v_mov_b32_e32 v8, 0
	s_and_saveexec_b64 s[2:3], vcc
	s_cbranch_execz .LBB0_2972
	v_mov_b32_e32 v8, v225
	s_nop 0
	v_lshlrev_b32_e32 v8, 16, v8
.LBB0_2972:
	s_or_b64 exec, exec, s[2:3]
	v_add_co_u32_e32 v24, vcc, 0x7000, v20
	s_movk_i32 s2, 0x3ff
	s_nop 0
	v_addc_co_u32_e32 v25, vcc, 0, v21, vcc
	v_mov_b32_e32 v9, v226
	v_cmp_gt_i32_e32 vcc, s2, v14
	s_and_saveexec_b64 s[2:3], vcc
	s_cbranch_execz .LBB0_2974
	s_mov_b64 s[6:7], 0x7800
	v_mov_b32_e32 v7, v227
	s_nop 0
	v_lshlrev_b32_e32 v7, 16, v7

.LBB0_2978:
	v_add_co_u32_e32 v4, vcc, 0xf000, v22
	s_movk_i32 s2, 0xc200
	s_nop 0
	v_addc_co_u32_e32 v5, vcc, 0, v23, vcc
	v_mov_b32_e32 v6, v229
	v_add_u32_e32 v4, 0x3e00, v14
	v_ashrrev_i32_e32 v5, 31, v4
	v_cmp_lt_i32_e32 vcc, s2, v14
	v_mov_b32_e32 v7, 0
	v_mov_b32_e32 v8, 0
	s_and_saveexec_b64 s[2:3], vcc
	s_cbranch_execz .LBB0_2980
	v_mov_b32_e32 v8, v230
	s_nop 0
	v_lshlrev_b32_e32 v8, 16, v8
.LBB0_2980:
	s_or_b64 exec, exec, s[2:3]
	v_add_co_u32_e32 v22, vcc, 0x7000, v20
	s_movk_i32 s0, 0x1ff
	s_nop 0
	v_addc_co_u32_e32 v23, vcc, 0, v21, vcc
	v_mov_b32_e32 v9, v231
	v_cmp_gt_i32_e32 vcc, s0, v14
	s_and_saveexec_b64 s[0:1], vcc
	s_cbranch_execz .LBB0_2982
	s_mov_b64 s[2:3], 0x7c00
	v_mov_b32_e32 v7, v232
	s_nop 0
	v_lshlrev_b32_e32 v7, 16, v7
